# FFT passes: fold sign-flip/swap register pair building (v_xor+v_mov) into op_sel/neg modifiers of the consuming packed f32 ops (extended liveness)
# speedup vs baseline: 1.0583x; 1.0234x over previous
.LBB0_634:
	s_or_b64 exec, exec, s[0:1]
	v_readlane_b32 s0, v251, 28
	v_mov_b32_e32 v90, v173
	v_mov_b32_e32 v2, s0
	v_readlane_b32 s0, v251, 34
	v_mov_b32_e32 v10, v1
	s_waitcnt lgkmcnt(0)
	v_mov_b32_e32 v3, s0
	s_barrier
	ds_read_b128 v[6:9], v2
	ds_read_b128 v[2:5], v3
	v_mov_b32_e32 v60, v164
	v_mov_b32_e32 v34, v165
	v_mov_b32_e32 v62, v166
	v_mov_b32_e32 v32, v167
	v_mov_b32_e32 v64, v168
	v_mov_b32_e32 v38, v169
	v_mov_b32_e32 v66, v170
	v_mov_b32_e32 v10, v171
	v_pk_add_f32 v[68:69], v[14:15], v[42:43]
	v_pk_add_f32 v[14:15], v[14:15], v[42:43] neg_lo:[0,1] neg_hi:[0,1]
	s_nop 0
	v_mov_b32_e32 v13, v15
	v_mov_b32_e32 v10, v14
	v_mov_b32_e32 v42, v15
	v_mov_b32_e32 v43, v11
	v_pk_mul_f32 v[14:15], v[12:13], v[66:67] op_sel_hi:[1,0] neg_lo:[0,1] neg_hi:[0,1]
	v_pk_add_f32 v[70:71], v[18:19], v[52:53]
	v_pk_fma_f32 v[42:43], v[42:43], v[60:61], v[14:15] op_sel_hi:[1,0,1]
	v_pk_add_f32 v[14:15], v[16:17], v[48:49]
	v_pk_add_f32 v[48:49], v[16:17], v[48:49] neg_lo:[0,1] neg_hi:[0,1]
	v_mov_b32_e32 v17, v11
	v_mov_b32_e32 v13, v48
	v_mov_b32_e32 v16, v48
	v_pk_mul_f32 v[54:55], v[12:13], v[38:39] op_sel_hi:[1,0] neg_lo:[0,1] neg_hi:[0,1]
	v_mov_b32_e32 v13, v49
	v_pk_add_f32 v[18:19], v[18:19], v[52:53] neg_lo:[0,1] neg_hi:[0,1]
	v_pk_fma_f32 v[16:17], v[16:17], v[34:35], v[54:55] op_sel_hi:[1,0,1]
	v_mov_b32_e32 v54, v49
	v_mov_b32_e32 v55, v11
	v_pk_mul_f32 v[48:49], v[12:13], v[64:65] op_sel_hi:[1,0] neg_lo:[0,1] neg_hi:[0,1]
	v_mov_b32_e32 v13, v18
	v_pk_fma_f32 v[48:49], v[54:55], v[62:63], v[48:49] op_sel_hi:[1,0,1]
	v_mov_b32_e32 v52, v18
	v_mov_b32_e32 v53, v11
	v_pk_mul_f32 v[54:55], v[12:13], v[32:33] op_sel_hi:[1,0] neg_lo:[0,1] neg_hi:[0,1]
	v_mov_b32_e32 v13, v19
	v_pk_fma_f32 v[52:53], v[52:53], v[32:33], v[54:55] op_sel_hi:[1,0,1]
	v_mov_b32_e32 v54, v19
	v_mov_b32_e32 v55, v11
	v_pk_add_f32 v[18:19], v[20:21], v[50:51]
	v_pk_add_f32 v[20:21], v[20:21], v[50:51] neg_lo:[0,1] neg_hi:[0,1]
	v_pk_mul_f32 v[54:55], v[54:55], v[64:65] op_sel_hi:[1,0]
	v_mov_b32_e32 v50, v20
	v_mov_b32_e32 v51, v11
	v_pk_fma_f32 v[54:55], v[12:13], v[62:63], v[54:55] op_sel_hi:[1,0,1] neg_lo:[0,1,0] neg_hi:[0,1,0]
	v_pk_mul_f32 v[50:51], v[50:51], v[38:39] op_sel_hi:[1,0]
	v_mov_b32_e32 v13, v20
	v_pk_fma_f32 v[58:59], v[12:13], v[34:35], v[50:51] op_sel_hi:[1,0,1] neg_lo:[0,1,0] neg_hi:[0,1,0]
	v_mov_b32_e32 v50, v21
	v_mov_b32_e32 v51, v11
	v_pk_mul_f32 v[50:51], v[50:51], v[66:67] op_sel_hi:[1,0]
	v_mov_b32_e32 v13, v21
	v_pk_add_f32 v[20:21], v[26:27], v[46:47]
	v_pk_add_f32 v[26:27], v[26:27], v[46:47] neg_lo:[0,1] neg_hi:[0,1]
	v_pk_fma_f32 v[56:57], v[12:13], v[60:61], v[50:51] op_sel_hi:[1,0,1] neg_lo:[0,1,0] neg_hi:[0,1,0]
	v_xor_b32_e32 v73, 0x80000000, v26
	v_mov_b32_e32 v46, v27
	v_mov_b32_e32 v47, v11
	v_mov_b32_e32 v13, v27
	v_pk_add_f32 v[26:27], v[30:31], v[44:45]
	v_pk_add_f32 v[30:31], v[30:31], v[44:45] neg_lo:[0,1] neg_hi:[0,1]
	v_pk_mul_f32 v[46:47], v[46:47], v[66:67] op_sel_hi:[1,0] neg_lo:[0,1] neg_hi:[0,1]
	v_mov_b32_e32 v44, v30
	v_mov_b32_e32 v45, v11
	v_pk_fma_f32 v[74:75], v[12:13], v[60:61], v[46:47] op_sel_hi:[1,0,1] neg_lo:[0,1,0] neg_hi:[0,1,0]
	v_pk_mul_f32 v[44:45], v[44:45], v[38:39] op_sel_hi:[1,0] neg_lo:[0,1] neg_hi:[0,1]
	v_mov_b32_e32 v13, v30
	v_pk_fma_f32 v[76:77], v[12:13], v[34:35], v[44:45] op_sel_hi:[1,0,1] neg_lo:[0,1,0] neg_hi:[0,1,0]
	v_mov_b32_e32 v44, v31
	v_mov_b32_e32 v45, v11
	v_pk_mul_f32 v[44:45], v[44:45], v[64:65] op_sel_hi:[1,0] neg_lo:[0,1] neg_hi:[0,1]
	v_mov_b32_e32 v13, v31
	v_pk_add_f32 v[30:31], v[28:29], v[40:41]
	v_pk_add_f32 v[28:29], v[28:29], v[40:41] neg_lo:[0,1] neg_hi:[0,1]
	v_pk_fma_f32 v[78:79], v[12:13], v[62:63], v[44:45] op_sel_hi:[1,0,1] neg_lo:[0,1,0] neg_hi:[0,1,0]
	v_mov_b32_e32 v13, v28
	v_mov_b32_e32 v40, v28
	v_mov_b32_e32 v41, v11
	v_pk_mul_f32 v[44:45], v[12:13], v[32:33] op_sel_hi:[1,0] neg_lo:[0,1] neg_hi:[0,1]
	v_mov_b32_e32 v13, v29
	v_pk_fma_f32 v[80:81], v[40:41], v[32:33], v[44:45] op_sel_hi:[1,0,1] neg_lo:[0,1,0] neg_hi:[0,1,0]
	v_mov_b32_e32 v40, v29
	v_pk_mul_f32 v[28:29], v[12:13], v[64:65] op_sel_hi:[1,0] neg_lo:[0,1] neg_hi:[0,1]
	v_mov_b32_e32 v45, v11
	v_pk_fma_f32 v[62:63], v[40:41], v[62:63], v[28:29] op_sel_hi:[1,0,1] neg_lo:[0,1,0] neg_hi:[0,1,0]
	v_pk_add_f32 v[28:29], v[24:25], v[36:37]
	v_pk_add_f32 v[24:25], v[24:25], v[36:37] neg_lo:[0,1] neg_hi:[0,1]
	v_mov_b32_e32 v37, v11
	v_mov_b32_e32 v13, v24
	v_mov_b32_e32 v36, v24
	v_pk_mul_f32 v[40:41], v[12:13], v[38:39] op_sel_hi:[1,0] neg_lo:[0,1] neg_hi:[0,1]
	v_mov_b32_e32 v13, v25
	v_pk_fma_f32 v[64:65], v[36:37], v[34:35], v[40:41] op_sel_hi:[1,0,1] neg_lo:[0,1,0] neg_hi:[0,1,0]
	v_mov_b32_e32 v36, v25
	v_pk_mul_f32 v[24:25], v[12:13], v[66:67] op_sel_hi:[1,0] neg_lo:[0,1] neg_hi:[0,1]
	v_mov_b32_e32 v41, v11
	v_pk_fma_f32 v[66:67], v[36:37], v[60:61], v[24:25] op_sel_hi:[1,0,1] neg_lo:[0,1,0] neg_hi:[0,1,0]
	v_pk_add_f32 v[24:25], v[68:69], v[20:21] neg_lo:[0,1] neg_hi:[0,1]
	v_pk_add_f32 v[20:21], v[68:69], v[20:21]
	v_mov_b32_e32 v13, v25
	v_mov_b32_e32 v36, v24
	v_mov_b32_e32 v40, v25
	v_pk_mul_f32 v[24:25], v[12:13], v[38:39] op_sel_hi:[1,0] neg_lo:[0,1] neg_hi:[0,1]
	v_mov_b32_e32 v69, v11
	v_pk_fma_f32 v[24:25], v[40:41], v[34:35], v[24:25] op_sel_hi:[1,0,1]
	v_pk_add_f32 v[40:41], v[14:15], v[26:27] neg_lo:[0,1] neg_hi:[0,1]
	v_pk_add_f32 v[14:15], v[14:15], v[26:27]
	v_mov_b32_e32 v13, v40
	v_mov_b32_e32 v44, v40
	v_pk_mul_f32 v[46:47], v[12:13], v[32:33] op_sel_hi:[1,0] neg_lo:[0,1] neg_hi:[0,1]
	v_mov_b32_e32 v13, v41
	v_pk_fma_f32 v[44:45], v[44:45], v[32:33], v[46:47] op_sel_hi:[1,0,1]
	v_mov_b32_e32 v46, v41
	v_mov_b32_e32 v47, v11
	v_pk_mul_f32 v[46:47], v[46:47], v[38:39] op_sel_hi:[1,0]
	v_pk_add_f32 v[40:41], v[70:71], v[30:31] neg_lo:[0,1] neg_hi:[0,1]
	v_pk_fma_f32 v[50:51], v[12:13], v[34:35], v[46:47] op_sel_hi:[1,0,1] neg_lo:[0,1,0] neg_hi:[0,1,0]
	v_mov_b32_e32 v46, v41
	v_mov_b32_e32 v47, v11
	v_xor_b32_e32 v83, 0x80000000, v40
	v_pk_mul_f32 v[46:47], v[46:47], v[38:39] op_sel_hi:[1,0] neg_lo:[0,1] neg_hi:[0,1]
	v_mov_b32_e32 v13, v41
	v_pk_add_f32 v[40:41], v[18:19], v[28:29] neg_lo:[0,1] neg_hi:[0,1]
	v_pk_fma_f32 v[84:85], v[12:13], v[34:35], v[46:47] op_sel_hi:[1,0,1] neg_lo:[0,1,0] neg_hi:[0,1,0]
	v_mov_b32_e32 v13, v40
	v_pk_add_f32 v[26:27], v[70:71], v[30:31]
	v_mov_b32_e32 v46, v40
	v_mov_b32_e32 v47, v11
	v_pk_mul_f32 v[60:61], v[12:13], v[32:33] op_sel_hi:[1,0] neg_lo:[0,1] neg_hi:[0,1]
	v_mov_b32_e32 v13, v41
	v_pk_add_f32 v[18:19], v[18:19], v[28:29]
	v_pk_add_f32 v[28:29], v[20:21], v[26:27] neg_lo:[0,1] neg_hi:[0,1]
	v_pk_fma_f32 v[86:87], v[46:47], v[32:33], v[60:61] op_sel_hi:[1,0,1] neg_lo:[0,1,0] neg_hi:[0,1,0]
	v_mov_b32_e32 v46, v41
	v_pk_mul_f32 v[40:41], v[12:13], v[38:39] op_sel_hi:[1,0] neg_lo:[0,1] neg_hi:[0,1]
	v_mov_b32_e32 v13, v29
	v_pk_fma_f32 v[88:89], v[46:47], v[34:35], v[40:41] op_sel_hi:[1,0,1] neg_lo:[0,1,0] neg_hi:[0,1,0]
	v_mov_b32_e32 v40, v28
	v_pk_add_f32 v[20:21], v[20:21], v[26:27]
	v_mov_b32_e32 v26, v29
	v_mov_b32_e32 v27, v11
	v_pk_mul_f32 v[28:29], v[12:13], v[32:33] op_sel_hi:[1,0] neg_lo:[0,1] neg_hi:[0,1]
	v_mov_b32_e32 v41, v11
	v_pk_fma_f32 v[26:27], v[26:27], v[32:33], v[28:29] op_sel_hi:[1,0,1]
	v_pk_add_f32 v[28:29], v[14:15], v[18:19] neg_lo:[0,1] neg_hi:[0,1]
	v_pk_add_f32 v[14:15], v[14:15], v[18:19]
	v_mov_b32_e32 v13, v29
	v_xor_b32_e32 v61, 0x80000000, v28
	v_mov_b32_e32 v18, v29
	v_mov_b32_e32 v19, v11
	v_pk_mul_f32 v[28:29], v[12:13], v[32:33] op_sel_hi:[1,0] neg_lo:[0,1] neg_hi:[0,1]
	v_pk_add_f32 v[30:31], v[20:21], v[14:15]
	v_pk_fma_f32 v[18:19], v[18:19], v[32:33], v[28:29] op_sel_hi:[1,0,1] neg_lo:[0,1,0] neg_hi:[0,1,0]
	v_pk_add_f32 v[28:29], v[20:21], v[14:15] neg_lo:[0,1] neg_hi:[0,1]
	v_mov_b32_e32 v60, v11
	v_pk_add_f32 v[14:15], v[28:29], 0 neg_lo:[1,1] neg_hi:[1,1]
	v_mov_b32_e32 v68, v28
	v_mov_b32_e32 v14, v11
	v_pk_add_f32 v[46:47], v[68:69], v[14:15]
	v_pk_add_f32 v[20:21], v[68:69], v[14:15] neg_lo:[0,1] neg_hi:[0,1]
	v_pk_add_f32 v[14:15], v[40:41], v[60:61]
	v_pk_add_f32 v[28:29], v[40:41], v[60:61] neg_lo:[0,1] neg_hi:[0,1]
	v_pk_add_f32 v[40:41], v[26:27], v[18:19]
	v_pk_add_f32 v[18:19], v[26:27], v[18:19] neg_lo:[0,1] neg_hi:[0,1]
	v_mov_b32_e32 v82, v11
	v_pk_add_f32 v[60:61], v[14:15], v[40:41]
	v_pk_add_f32 v[26:27], v[14:15], v[40:41] neg_lo:[0,1] neg_hi:[0,1]
	v_pk_add_f32 v[40:41], v[28:29], v[18:19] op_sel:[0,1] op_sel_hi:[1,0] neg_hi:[0,1]
	v_pk_add_f32 v[14:15], v[28:29], v[18:19] op_sel:[0,1] op_sel_hi:[1,0] neg_lo:[0,1]
	v_pk_add_f32 v[18:19], v[36:37], v[82:83]
	v_pk_add_f32 v[28:29], v[36:37], v[82:83] neg_lo:[0,1] neg_hi:[0,1]
	v_pk_add_f32 v[36:37], v[24:25], v[84:85]
	v_pk_add_f32 v[24:25], v[24:25], v[84:85] neg_lo:[0,1] neg_hi:[0,1]
	v_mov_b32_e32 v72, v11
	v_pk_mul_f32 v[68:69], v[32:33], v[24:25] op_sel:[0,1] op_sel_hi:[0,0] neg_lo:[1,1] neg_hi:[1,0]
	v_pk_fma_f32 v[68:69], v[32:33], v[24:25], v[68:69] op_sel_hi:[0,1,1]
	v_pk_add_f32 v[24:25], v[44:45], v[86:87]
	v_pk_add_f32 v[44:45], v[44:45], v[86:87] neg_lo:[0,1] neg_hi:[0,1]
	v_lshl_add_u32 v13, v90, 3, 0
	v_xor_b32_e32 v71, 0x80000000, v44
	v_mov_b32_e32 v70, v45
	v_pk_add_f32 v[44:45], v[50:51], v[88:89]
	v_pk_add_f32 v[50:51], v[50:51], v[88:89] neg_lo:[0,1] neg_hi:[0,1]
	s_nop 0
	v_pk_mul_f32 v[82:83], v[32:33], v[50:51] op_sel:[0,1] op_sel_hi:[0,0] neg_lo:[1,1] neg_hi:[1,0]
	v_pk_fma_f32 v[82:83], v[32:33], v[50:51], v[82:83] op_sel_hi:[0,1,1] neg_lo:[1,0,0] neg_hi:[1,0,0]
	v_pk_add_f32 v[50:51], v[18:19], v[24:25]
	v_pk_add_f32 v[18:19], v[18:19], v[24:25] neg_lo:[0,1] neg_hi:[0,1]
	v_pk_add_f32 v[24:25], v[36:37], v[44:45]
	v_pk_add_f32 v[36:37], v[36:37], v[44:45] neg_lo:[0,1] neg_hi:[0,1]
	v_pk_add_f32 v[84:85], v[50:51], v[24:25]
	v_xor_b32_e32 v45, 0x80000000, v36
	v_mov_b32_e32 v44, v37
	v_pk_add_f32 v[36:37], v[50:51], v[24:25] neg_lo:[0,1] neg_hi:[0,1]
	v_pk_add_f32 v[50:51], v[18:19], v[44:45]
	v_pk_add_f32 v[24:25], v[18:19], v[44:45] neg_lo:[0,1] neg_hi:[0,1]
	v_pk_add_f32 v[44:45], v[68:69], v[82:83] neg_lo:[0,1] neg_hi:[0,1]
	v_pk_add_f32 v[18:19], v[28:29], v[70:71]
	v_pk_add_f32 v[70:71], v[28:29], v[70:71] neg_lo:[0,1] neg_hi:[0,1]
	v_pk_add_f32 v[28:29], v[68:69], v[82:83]
	v_xor_b32_e32 v69, 0x80000000, v44
	v_mov_b32_e32 v68, v45
	v_pk_add_f32 v[82:83], v[18:19], v[28:29]
	v_pk_add_f32 v[28:29], v[18:19], v[28:29] neg_lo:[0,1] neg_hi:[0,1]
	v_pk_add_f32 v[44:45], v[70:71], v[68:69]
	v_pk_add_f32 v[18:19], v[70:71], v[68:69] neg_lo:[0,1] neg_hi:[0,1]
	v_pk_add_f32 v[68:69], v[10:11], v[72:73]
	v_pk_add_f32 v[70:71], v[10:11], v[72:73] neg_lo:[0,1] neg_hi:[0,1]
	v_pk_add_f32 v[72:73], v[42:43], v[74:75]
	v_pk_add_f32 v[42:43], v[42:43], v[74:75] neg_lo:[0,1] neg_hi:[0,1]
	v_add_f32_e32 v10, v30, v31
	v_pk_mul_f32 v[74:75], v[38:39], v[42:43] op_sel:[0,1] op_sel_hi:[0,0] neg_lo:[1,1] neg_hi:[1,0]
	v_pk_fma_f32 v[42:43], v[34:35], v[42:43], v[74:75] op_sel_hi:[0,1,1]
	v_pk_add_f32 v[74:75], v[16:17], v[76:77]
	v_pk_add_f32 v[16:17], v[16:17], v[76:77] neg_lo:[0,1] neg_hi:[0,1]
	s_nop 0
	v_pk_mul_f32 v[76:77], v[32:33], v[16:17] op_sel:[0,1] op_sel_hi:[0,0] neg_lo:[1,1] neg_hi:[1,0]
	v_pk_fma_f32 v[16:17], v[32:33], v[16:17], v[76:77] op_sel_hi:[0,1,1]
	v_pk_add_f32 v[76:77], v[48:49], v[78:79]
	v_pk_add_f32 v[48:49], v[48:49], v[78:79] neg_lo:[0,1] neg_hi:[0,1]
	s_nop 0
	v_pk_mul_f32 v[78:79], v[34:35], v[48:49] op_sel:[0,1] op_sel_hi:[0,0] neg_lo:[1,1] neg_hi:[1,0]
	v_pk_fma_f32 v[78:79], v[38:39], v[48:49], v[78:79] op_sel_hi:[0,1,1]
	v_pk_add_f32 v[48:49], v[52:53], v[80:81]
	v_pk_add_f32 v[52:53], v[52:53], v[80:81] neg_lo:[0,1] neg_hi:[0,1]
	s_nop 0
	v_xor_b32_e32 v81, 0x80000000, v52
	v_mov_b32_e32 v80, v53
	v_pk_add_f32 v[52:53], v[54:55], v[62:63]
	v_pk_add_f32 v[54:55], v[54:55], v[62:63] neg_lo:[0,1] neg_hi:[0,1]
	s_nop 0
	v_pk_mul_f32 v[62:63], v[34:35], v[54:55] op_sel:[0,1] op_sel_hi:[0,0] neg_lo:[1,1] neg_hi:[1,0]
	v_pk_fma_f32 v[62:63], v[38:39], v[54:55], v[62:63] op_sel_hi:[0,1,1] neg_lo:[1,0,0] neg_hi:[1,0,0]
	v_pk_add_f32 v[54:55], v[58:59], v[64:65]
	v_pk_add_f32 v[58:59], v[58:59], v[64:65] neg_lo:[0,1] neg_hi:[0,1]
	s_nop 0
	v_pk_mul_f32 v[64:65], v[32:33], v[58:59] op_sel:[0,1] op_sel_hi:[0,0] neg_lo:[1,1] neg_hi:[1,0]
	v_pk_fma_f32 v[58:59], v[32:33], v[58:59], v[64:65] op_sel_hi:[0,1,1] neg_lo:[1,0,0] neg_hi:[1,0,0]
	v_pk_add_f32 v[64:65], v[56:57], v[66:67]
	v_pk_add_f32 v[56:57], v[56:57], v[66:67] neg_lo:[0,1] neg_hi:[0,1]
	s_nop 0
	v_pk_mul_f32 v[38:39], v[38:39], v[56:57] op_sel:[0,1] op_sel_hi:[0,0] neg_lo:[1,1] neg_hi:[1,0]
	v_pk_fma_f32 v[56:57], v[34:35], v[56:57], v[38:39] op_sel_hi:[0,1,1] neg_lo:[1,0,0] neg_hi:[1,0,0]
	v_pk_add_f32 v[38:39], v[52:53], v[72:73]
	v_pk_add_f32 v[52:53], v[72:73], v[52:53] neg_lo:[0,1] neg_hi:[0,1]
	v_pk_add_f32 v[34:35], v[68:69], v[48:49]
	v_pk_mul_f32 v[66:67], v[32:33], v[52:53] op_sel:[0,1] op_sel_hi:[0,0] neg_lo:[1,1] neg_hi:[1,0]
	v_pk_fma_f32 v[52:53], v[32:33], v[52:53], v[66:67] op_sel_hi:[0,1,1]
	v_pk_add_f32 v[66:67], v[74:75], v[54:55]
	v_pk_add_f32 v[54:55], v[74:75], v[54:55] neg_lo:[0,1] neg_hi:[0,1]
	v_pk_add_f32 v[48:49], v[68:69], v[48:49] neg_lo:[0,1] neg_hi:[0,1]
	v_xor_b32_e32 v69, 0x80000000, v54
	v_mov_b32_e32 v68, v55
	v_pk_add_f32 v[54:55], v[76:77], v[64:65]
	v_pk_add_f32 v[64:65], v[76:77], v[64:65] neg_lo:[0,1] neg_hi:[0,1]
	s_nop 0
	v_pk_mul_f32 v[72:73], v[32:33], v[64:65] op_sel:[0,1] op_sel_hi:[0,0] neg_lo:[1,1] neg_hi:[1,0]
	v_pk_fma_f32 v[64:65], v[32:33], v[64:65], v[72:73] op_sel_hi:[0,1,1] neg_lo:[1,0,0] neg_hi:[1,0,0]
	v_pk_add_f32 v[72:73], v[34:35], v[66:67]
	v_pk_add_f32 v[34:35], v[34:35], v[66:67] neg_lo:[0,1] neg_hi:[0,1]
	v_pk_add_f32 v[66:67], v[38:39], v[54:55]
	v_pk_add_f32 v[38:39], v[38:39], v[54:55] neg_lo:[0,1] neg_hi:[0,1]
	v_pk_add_f32 v[76:77], v[72:73], v[66:67]
	v_pk_add_f32 v[54:55], v[72:73], v[66:67] neg_lo:[0,1] neg_hi:[0,1]
	v_pk_add_f32 v[66:67], v[34:35], v[38:39] op_sel:[0,1] op_sel_hi:[1,0] neg_hi:[0,1]
	v_pk_add_f32 v[38:39], v[34:35], v[38:39] op_sel:[0,1] op_sel_hi:[1,0] neg_lo:[0,1]
	v_pk_add_f32 v[34:35], v[48:49], v[68:69]
	v_pk_add_f32 v[68:69], v[48:49], v[68:69] neg_lo:[0,1] neg_hi:[0,1]
	v_pk_add_f32 v[48:49], v[52:53], v[64:65]
	v_pk_add_f32 v[52:53], v[52:53], v[64:65] neg_lo:[0,1] neg_hi:[0,1]
	v_pk_add_f32 v[72:73], v[34:35], v[48:49]
	v_pk_add_f32 v[48:49], v[34:35], v[48:49] neg_lo:[0,1] neg_hi:[0,1]
	v_pk_add_f32 v[74:75], v[68:69], v[52:53] op_sel:[0,1] op_sel_hi:[1,0] neg_hi:[0,1]
	v_pk_add_f32 v[34:35], v[68:69], v[52:53] op_sel:[0,1] op_sel_hi:[1,0] neg_lo:[0,1]
	v_pk_add_f32 v[68:69], v[62:63], v[42:43]
	v_pk_add_f32 v[42:43], v[42:43], v[62:63] neg_lo:[0,1] neg_hi:[0,1]
	v_pk_add_f32 v[52:53], v[70:71], v[80:81]
	v_pk_mul_f32 v[62:63], v[32:33], v[42:43] op_sel:[0,1] op_sel_hi:[0,0] neg_lo:[1,1] neg_hi:[1,0]
	v_pk_fma_f32 v[62:63], v[32:33], v[42:43], v[62:63] op_sel_hi:[0,1,1]
	v_pk_add_f32 v[42:43], v[16:17], v[58:59]
	v_pk_add_f32 v[16:17], v[16:17], v[58:59] neg_lo:[0,1] neg_hi:[0,1]
	v_pk_add_f32 v[64:65], v[70:71], v[80:81] neg_lo:[0,1] neg_hi:[0,1]
	v_xor_b32_e32 v59, 0x80000000, v16
	v_mov_b32_e32 v58, v17
	v_pk_add_f32 v[16:17], v[78:79], v[56:57]
	v_pk_add_f32 v[56:57], v[78:79], v[56:57] neg_lo:[0,1] neg_hi:[0,1]
	s_nop 0
	v_pk_mul_f32 v[70:71], v[32:33], v[56:57] op_sel:[0,1] op_sel_hi:[0,0] neg_lo:[1,1] neg_hi:[1,0]
	v_pk_fma_f32 v[32:33], v[32:33], v[56:57], v[70:71] op_sel_hi:[0,1,1] neg_lo:[1,0,0] neg_hi:[1,0,0]
	v_pk_add_f32 v[56:57], v[52:53], v[42:43]
	v_pk_add_f32 v[42:43], v[52:53], v[42:43] neg_lo:[0,1] neg_hi:[0,1]
	v_pk_add_f32 v[52:53], v[68:69], v[16:17]
	v_pk_add_f32 v[16:17], v[68:69], v[16:17] neg_lo:[0,1] neg_hi:[0,1]
	v_pk_add_f32 v[70:71], v[56:57], v[52:53]
	v_xor_b32_e32 v69, 0x80000000, v16
	v_mov_b32_e32 v68, v17
	v_pk_add_f32 v[56:57], v[56:57], v[52:53] neg_lo:[0,1] neg_hi:[0,1]
	v_pk_add_f32 v[16:17], v[64:65], v[58:59]
	v_pk_add_f32 v[52:53], v[62:63], v[32:33]
	v_pk_add_f32 v[32:33], v[62:63], v[32:33] neg_lo:[0,1] neg_hi:[0,1]
	v_pk_add_f32 v[58:59], v[64:65], v[58:59] neg_lo:[0,1] neg_hi:[0,1]
	v_pk_add_f32 v[64:65], v[16:17], v[52:53]
	v_pk_add_f32 v[52:53], v[16:17], v[52:53] neg_lo:[0,1] neg_hi:[0,1]
	v_mov_b64_e32 v[16:17], s[90:91]
	v_pk_add_f32 v[78:79], v[42:43], v[68:69]
	v_pk_add_f32 v[42:43], v[42:43], v[68:69] neg_lo:[0,1] neg_hi:[0,1]
	v_pk_add_f32 v[68:69], v[58:59], v[32:33] op_sel:[0,1] op_sel_hi:[1,0] neg_hi:[0,1]
	v_pk_add_f32 v[32:33], v[58:59], v[32:33] op_sel:[0,1] op_sel_hi:[1,0] neg_lo:[0,1]
	v_pk_fma_f32 v[58:59], v[10:11], s[94:95], v[16:17] op_sel_hi:[0,1,1]
	ds_write_b64 v13, v[58:59]
	v_pk_fma_f32 v[58:59], v[178:179], s[90:91], v[178:179] op_sel:[1,0,0] op_sel_hi:[0,1,1]
	v_pk_mul_f32 v[62:63], v[58:59], v[76:77] op_sel:[1,1] op_sel_hi:[0,1] neg_lo:[0,1]
	v_pk_fma_f32 v[62:63], v[58:59], v[76:77], v[62:63] op_sel_hi:[1,0,1]
	ds_write_b64 v13, v[62:63] offset:4224
	v_pk_mul_f32 v[62:63], v[178:179], v[58:59] op_sel:[1,1] op_sel_hi:[0,1] neg_lo:[0,1]
	v_pk_fma_f32 v[58:59], v[178:179], v[58:59], v[62:63] op_sel_hi:[1,0,1]
	s_nop 0
	v_pk_mul_f32 v[62:63], v[58:59], v[84:85] op_sel:[1,1] op_sel_hi:[0,1] neg_lo:[0,1]
	v_pk_fma_f32 v[62:63], v[58:59], v[84:85], v[62:63] op_sel_hi:[1,0,1]
	ds_write_b64 v13, v[62:63] offset:8448
	v_pk_mul_f32 v[62:63], v[178:179], v[58:59] op_sel:[1,1] op_sel_hi:[0,1] neg_lo:[0,1]
	v_pk_fma_f32 v[58:59], v[178:179], v[58:59], v[62:63] op_sel_hi:[1,0,1]
	s_nop 0
	v_pk_mul_f32 v[62:63], v[58:59], v[70:71] op_sel:[1,1] op_sel_hi:[0,1] neg_lo:[0,1]
	v_pk_fma_f32 v[62:63], v[58:59], v[70:71], v[62:63] op_sel_hi:[1,0,1]
	ds_write_b64 v13, v[62:63] offset:12672
	v_pk_mul_f32 v[62:63], v[178:179], v[58:59] op_sel:[1,1] op_sel_hi:[0,1] neg_lo:[0,1]
	v_pk_fma_f32 v[58:59], v[178:179], v[58:59], v[62:63] op_sel_hi:[1,0,1]
	s_nop 0
	v_pk_mul_f32 v[62:63], v[60:61], v[58:59] op_sel:[1,1] op_sel_hi:[1,0] neg_lo:[1,0]
	s_nop 0
	v_pk_fma_f32 v[60:61], v[60:61], v[58:59], v[62:63] op_sel_hi:[0,1,1]
	ds_write_b64 v13, v[60:61] offset:16896
	v_pk_mul_f32 v[60:61], v[178:179], v[58:59] op_sel:[1,1] op_sel_hi:[0,1] neg_lo:[0,1]
	v_pk_fma_f32 v[58:59], v[178:179], v[58:59], v[60:61] op_sel_hi:[1,0,1]
	s_nop 0
	v_pk_mul_f32 v[60:61], v[58:59], v[72:73] op_sel:[1,1] op_sel_hi:[0,1] neg_lo:[0,1]
	v_pk_fma_f32 v[60:61], v[58:59], v[72:73], v[60:61] op_sel_hi:[1,0,1]
	ds_write_b64 v13, v[60:61] offset:21120
	v_pk_mul_f32 v[60:61], v[178:179], v[58:59] op_sel:[1,1] op_sel_hi:[0,1] neg_lo:[0,1]
	v_pk_fma_f32 v[58:59], v[178:179], v[58:59], v[60:61] op_sel_hi:[1,0,1]
	s_nop 0
	v_pk_mul_f32 v[60:61], v[82:83], v[58:59] op_sel:[1,1] op_sel_hi:[1,0] neg_lo:[1,0]
	s_nop 0
	v_pk_fma_f32 v[60:61], v[82:83], v[58:59], v[60:61] op_sel_hi:[0,1,1]
	ds_write_b64 v13, v[60:61] offset:25344
	v_pk_mul_f32 v[60:61], v[178:179], v[58:59] op_sel:[1,1] op_sel_hi:[0,1] neg_lo:[0,1]
	v_pk_fma_f32 v[58:59], v[178:179], v[58:59], v[60:61] op_sel_hi:[1,0,1]
	s_nop 0
	v_pk_mul_f32 v[60:61], v[64:65], v[58:59] op_sel:[1,1] op_sel_hi:[1,0] neg_lo:[1,0]
	s_nop 0
	v_pk_fma_f32 v[60:61], v[64:65], v[58:59], v[60:61] op_sel_hi:[0,1,1]
	ds_write_b64 v13, v[60:61] offset:29568
	v_pk_mul_f32 v[60:61], v[178:179], v[58:59] op_sel:[1,1] op_sel_hi:[0,1] neg_lo:[0,1]
	v_pk_fma_f32 v[58:59], v[178:179], v[58:59], v[60:61] op_sel_hi:[1,0,1]
	s_nop 0
	v_pk_mul_f32 v[60:61], v[46:47], v[58:59] op_sel:[1,1] op_sel_hi:[1,0] neg_lo:[1,0]
	s_nop 0
	v_pk_fma_f32 v[46:47], v[46:47], v[58:59], v[60:61] op_sel_hi:[0,1,1]
	ds_write_b64 v13, v[46:47] offset:33792
	v_pk_mul_f32 v[46:47], v[178:179], v[58:59] op_sel:[1,1] op_sel_hi:[0,1] neg_lo:[0,1]
	v_pk_fma_f32 v[46:47], v[178:179], v[58:59], v[46:47] op_sel_hi:[1,0,1]
	s_nop 0
	v_pk_mul_f32 v[58:59], v[66:67], v[46:47] op_sel:[1,1] op_sel_hi:[1,0] neg_lo:[1,0]
	s_nop 0
	v_pk_fma_f32 v[58:59], v[66:67], v[46:47], v[58:59] op_sel_hi:[0,1,1]
	ds_write_b64 v13, v[58:59] offset:38016
	v_pk_mul_f32 v[58:59], v[178:179], v[46:47] op_sel:[1,1] op_sel_hi:[0,1] neg_lo:[0,1]
	v_pk_fma_f32 v[46:47], v[178:179], v[46:47], v[58:59] op_sel_hi:[1,0,1]
	s_nop 0
	v_pk_mul_f32 v[58:59], v[50:51], v[46:47] op_sel:[1,1] op_sel_hi:[1,0] neg_lo:[1,0]
	s_nop 0
	v_pk_fma_f32 v[50:51], v[50:51], v[46:47], v[58:59] op_sel_hi:[0,1,1]
	ds_write_b64 v13, v[50:51] offset:42240
	v_pk_mul_f32 v[50:51], v[178:179], v[46:47] op_sel:[1,1] op_sel_hi:[0,1] neg_lo:[0,1]
	v_pk_fma_f32 v[46:47], v[178:179], v[46:47], v[50:51] op_sel_hi:[1,0,1]
	s_nop 0
	v_pk_mul_f32 v[50:51], v[78:79], v[46:47] op_sel:[1,1] op_sel_hi:[1,0] neg_lo:[1,0]
	s_nop 0
	v_pk_fma_f32 v[50:51], v[78:79], v[46:47], v[50:51] op_sel_hi:[0,1,1]
	ds_write_b64 v13, v[50:51] offset:46464
	v_pk_mul_f32 v[50:51], v[178:179], v[46:47] op_sel:[1,1] op_sel_hi:[0,1] neg_lo:[0,1]
	v_pk_fma_f32 v[46:47], v[178:179], v[46:47], v[50:51] op_sel_hi:[1,0,1]
	s_nop 0
	v_pk_mul_f32 v[50:51], v[40:41], v[46:47] op_sel:[1,1] op_sel_hi:[1,0] neg_lo:[1,0]
	s_nop 0
	v_pk_fma_f32 v[40:41], v[40:41], v[46:47], v[50:51] op_sel_hi:[0,1,1]
	ds_write_b64 v13, v[40:41] offset:50688
	v_pk_mul_f32 v[40:41], v[178:179], v[46:47] op_sel:[1,1] op_sel_hi:[0,1] neg_lo:[0,1]
	v_pk_fma_f32 v[40:41], v[178:179], v[46:47], v[40:41] op_sel_hi:[1,0,1]
	s_nop 0
	v_pk_mul_f32 v[46:47], v[74:75], v[40:41] op_sel:[1,1] op_sel_hi:[1,0] neg_lo:[1,0]
	s_nop 0
	v_pk_fma_f32 v[46:47], v[74:75], v[40:41], v[46:47] op_sel_hi:[0,1,1]
	ds_write_b64 v13, v[46:47] offset:54912
	v_pk_mul_f32 v[46:47], v[178:179], v[40:41] op_sel:[1,1] op_sel_hi:[0,1] neg_lo:[0,1]
	v_pk_fma_f32 v[40:41], v[178:179], v[40:41], v[46:47] op_sel_hi:[1,0,1]
	s_nop 0
	v_pk_mul_f32 v[46:47], v[44:45], v[40:41] op_sel:[1,1] op_sel_hi:[1,0] neg_lo:[1,0]
	s_nop 0
	v_pk_fma_f32 v[44:45], v[44:45], v[40:41], v[46:47] op_sel_hi:[0,1,1]
	ds_write_b64 v13, v[44:45] offset:59136
	v_pk_mul_f32 v[44:45], v[178:179], v[40:41] op_sel:[1,1] op_sel_hi:[0,1] neg_lo:[0,1]
	v_pk_fma_f32 v[40:41], v[178:179], v[40:41], v[44:45] op_sel_hi:[1,0,1]
	s_nop 0
	v_pk_mul_f32 v[44:45], v[68:69], v[40:41] op_sel:[1,1] op_sel_hi:[1,0] neg_lo:[1,0]
	s_nop 0
	v_pk_fma_f32 v[44:45], v[68:69], v[40:41], v[44:45] op_sel_hi:[0,1,1]
	ds_write_b64 v13, v[44:45] offset:63360
	v_pk_mul_f32 v[44:45], v[178:179], v[40:41] op_sel:[1,1] op_sel_hi:[0,1] neg_lo:[0,1]
	v_pk_fma_f32 v[40:41], v[178:179], v[40:41], v[44:45] op_sel_hi:[1,0,1]
	s_mov_b32 s44, s95
	v_sub_f32_e32 v10, v30, v31
	v_pk_mul_f32 v[30:31], v[40:41], s[44:45]
	s_nop 0
	v_pk_fma_f32 v[30:31], v[10:11], v[40:41], v[30:31] op_sel:[0,0,1] op_sel_hi:[0,1,0]
	v_add_u32_e32 v10, 0x10800, v13
	ds_write_b64 v10, v[30:31]
	v_pk_mul_f32 v[30:31], v[178:179], v[40:41] op_sel:[1,1] op_sel_hi:[0,1] neg_lo:[0,1]
	v_pk_fma_f32 v[30:31], v[178:179], v[40:41], v[30:31] op_sel_hi:[1,0,1]
	s_nop 0
	v_pk_mul_f32 v[40:41], v[54:55], v[30:31] op_sel:[1,1] op_sel_hi:[1,0] neg_lo:[1,0]
	v_add_u32_e32 v10, 0x11880, v13
	v_pk_fma_f32 v[40:41], v[54:55], v[30:31], v[40:41] op_sel_hi:[0,1,1]
	ds_write_b64 v10, v[40:41]
	v_pk_mul_f32 v[40:41], v[178:179], v[30:31] op_sel:[1,1] op_sel_hi:[0,1] neg_lo:[0,1]
	v_pk_fma_f32 v[30:31], v[178:179], v[30:31], v[40:41] op_sel_hi:[1,0,1]
	s_nop 0
	v_pk_mul_f32 v[40:41], v[36:37], v[30:31] op_sel:[1,1] op_sel_hi:[1,0] neg_lo:[1,0]
	v_add_u32_e32 v10, 0x12900, v13
	v_pk_fma_f32 v[36:37], v[36:37], v[30:31], v[40:41] op_sel_hi:[0,1,1]
	ds_write_b64 v10, v[36:37]
	v_pk_mul_f32 v[36:37], v[178:179], v[30:31] op_sel:[1,1] op_sel_hi:[0,1] neg_lo:[0,1]
	v_pk_fma_f32 v[30:31], v[178:179], v[30:31], v[36:37] op_sel_hi:[1,0,1]
	s_nop 0
	v_pk_mul_f32 v[36:37], v[56:57], v[30:31] op_sel:[1,1] op_sel_hi:[1,0] neg_lo:[1,0]
	v_add_u32_e32 v10, 0x13980, v13
	v_pk_fma_f32 v[36:37], v[56:57], v[30:31], v[36:37] op_sel_hi:[0,1,1]
	ds_write_b64 v10, v[36:37]
	v_pk_mul_f32 v[36:37], v[178:179], v[30:31] op_sel:[1,1] op_sel_hi:[0,1] neg_lo:[0,1]
	v_pk_fma_f32 v[30:31], v[178:179], v[30:31], v[36:37] op_sel_hi:[1,0,1]
	s_nop 0
	v_pk_mul_f32 v[36:37], v[26:27], v[30:31] op_sel:[1,1] op_sel_hi:[1,0] neg_lo:[1,0]
	v_add_u32_e32 v10, 0x14a00, v13
	v_pk_fma_f32 v[26:27], v[26:27], v[30:31], v[36:37] op_sel_hi:[0,1,1]
	ds_write_b64 v10, v[26:27]
	v_pk_mul_f32 v[26:27], v[178:179], v[30:31] op_sel:[1,1] op_sel_hi:[0,1] neg_lo:[0,1]
	v_pk_fma_f32 v[26:27], v[178:179], v[30:31], v[26:27] op_sel_hi:[1,0,1]
	s_nop 0
	v_pk_mul_f32 v[30:31], v[48:49], v[26:27] op_sel:[1,1] op_sel_hi:[1,0] neg_lo:[1,0]
	v_add_u32_e32 v10, 0x15a80, v13
	v_pk_fma_f32 v[30:31], v[48:49], v[26:27], v[30:31] op_sel_hi:[0,1,1]
	ds_write_b64 v10, v[30:31]
	v_pk_mul_f32 v[30:31], v[178:179], v[26:27] op_sel:[1,1] op_sel_hi:[0,1] neg_lo:[0,1]
	v_pk_fma_f32 v[26:27], v[178:179], v[26:27], v[30:31] op_sel_hi:[1,0,1]
	s_nop 0
	v_pk_mul_f32 v[30:31], v[28:29], v[26:27] op_sel:[1,1] op_sel_hi:[1,0] neg_lo:[1,0]
	v_add_u32_e32 v10, 0x16b00, v13
	v_pk_fma_f32 v[28:29], v[28:29], v[26:27], v[30:31] op_sel_hi:[0,1,1]
	ds_write_b64 v10, v[28:29]
	v_pk_mul_f32 v[28:29], v[178:179], v[26:27] op_sel:[1,1] op_sel_hi:[0,1] neg_lo:[0,1]
	v_pk_fma_f32 v[26:27], v[178:179], v[26:27], v[28:29] op_sel_hi:[1,0,1]
	s_nop 0
	v_pk_mul_f32 v[28:29], v[52:53], v[26:27] op_sel:[1,1] op_sel_hi:[1,0] neg_lo:[1,0]
	v_add_u32_e32 v10, 0x17b80, v13
	v_pk_fma_f32 v[28:29], v[52:53], v[26:27], v[28:29] op_sel_hi:[0,1,1]
	ds_write_b64 v10, v[28:29]
	v_pk_mul_f32 v[28:29], v[178:179], v[26:27] op_sel:[1,1] op_sel_hi:[0,1] neg_lo:[0,1]
	v_pk_fma_f32 v[26:27], v[178:179], v[26:27], v[28:29] op_sel_hi:[1,0,1]
	s_nop 0
	v_pk_mul_f32 v[28:29], v[20:21], v[26:27] op_sel:[1,1] op_sel_hi:[1,0] neg_lo:[1,0]
	v_add_u32_e32 v10, 0x18c00, v13
	v_pk_fma_f32 v[20:21], v[20:21], v[26:27], v[28:29] op_sel_hi:[0,1,1]
	ds_write_b64 v10, v[20:21]
	v_pk_mul_f32 v[20:21], v[178:179], v[26:27] op_sel:[1,1] op_sel_hi:[0,1] neg_lo:[0,1]
	v_pk_fma_f32 v[20:21], v[178:179], v[26:27], v[20:21] op_sel_hi:[1,0,1]
	s_nop 0
	v_pk_mul_f32 v[26:27], v[38:39], v[20:21] op_sel:[1,1] op_sel_hi:[1,0] neg_lo:[1,0]
	v_add_u32_e32 v10, 0x19c80, v13
	v_pk_fma_f32 v[26:27], v[38:39], v[20:21], v[26:27] op_sel_hi:[0,1,1]
	ds_write_b64 v10, v[26:27]
	v_pk_mul_f32 v[26:27], v[178:179], v[20:21] op_sel:[1,1] op_sel_hi:[0,1] neg_lo:[0,1]
	v_pk_fma_f32 v[20:21], v[178:179], v[20:21], v[26:27] op_sel_hi:[1,0,1]
	s_nop 0
	v_pk_mul_f32 v[26:27], v[24:25], v[20:21] op_sel:[1,1] op_sel_hi:[1,0] neg_lo:[1,0]
	v_add_u32_e32 v10, 0x1ad00, v13
	v_pk_fma_f32 v[24:25], v[24:25], v[20:21], v[26:27] op_sel_hi:[0,1,1]
	ds_write_b64 v10, v[24:25]
	v_pk_mul_f32 v[24:25], v[178:179], v[20:21] op_sel:[1,1] op_sel_hi:[0,1] neg_lo:[0,1]
	v_pk_fma_f32 v[20:21], v[178:179], v[20:21], v[24:25] op_sel_hi:[1,0,1]
	s_nop 0
	v_pk_mul_f32 v[24:25], v[42:43], v[20:21] op_sel:[1,1] op_sel_hi:[1,0] neg_lo:[1,0]
	v_add_u32_e32 v10, 0x1bd80, v13
	v_pk_fma_f32 v[24:25], v[42:43], v[20:21], v[24:25] op_sel_hi:[0,1,1]
	ds_write_b64 v10, v[24:25]
	v_pk_mul_f32 v[24:25], v[178:179], v[20:21] op_sel:[1,1] op_sel_hi:[0,1] neg_lo:[0,1]
	v_pk_fma_f32 v[20:21], v[178:179], v[20:21], v[24:25] op_sel_hi:[1,0,1]
	s_nop 0
	v_pk_mul_f32 v[24:25], v[14:15], v[20:21] op_sel:[1,1] op_sel_hi:[1,0] neg_lo:[1,0]
	v_add_u32_e32 v10, 0x1ce00, v13
	v_pk_fma_f32 v[14:15], v[14:15], v[20:21], v[24:25] op_sel_hi:[0,1,1]
	ds_write_b64 v10, v[14:15]
	v_pk_mul_f32 v[14:15], v[178:179], v[20:21] op_sel:[1,1] op_sel_hi:[0,1] neg_lo:[0,1]
	v_pk_fma_f32 v[14:15], v[178:179], v[20:21], v[14:15] op_sel_hi:[1,0,1]
	s_nop 0
	v_pk_mul_f32 v[20:21], v[34:35], v[14:15] op_sel:[1,1] op_sel_hi:[1,0] neg_lo:[1,0]
	v_add_u32_e32 v10, 0x1de80, v13
	v_pk_fma_f32 v[20:21], v[34:35], v[14:15], v[20:21] op_sel_hi:[0,1,1]
	ds_write_b64 v10, v[20:21]
	v_pk_mul_f32 v[20:21], v[178:179], v[14:15] op_sel:[1,1] op_sel_hi:[0,1] neg_lo:[0,1]
	v_pk_fma_f32 v[14:15], v[178:179], v[14:15], v[20:21] op_sel_hi:[1,0,1]
	s_nop 0
	v_pk_mul_f32 v[20:21], v[18:19], v[14:15] op_sel:[1,1] op_sel_hi:[1,0] neg_lo:[1,0]
	v_add_u32_e32 v10, 0x1ef00, v13
	v_pk_fma_f32 v[18:19], v[18:19], v[14:15], v[20:21] op_sel_hi:[0,1,1]
	ds_write_b64 v10, v[18:19]
	v_pk_mul_f32 v[18:19], v[178:179], v[14:15] op_sel:[1,1] op_sel_hi:[0,1] neg_lo:[0,1]
	v_pk_fma_f32 v[14:15], v[178:179], v[14:15], v[18:19] op_sel_hi:[1,0,1]
	s_nop 0
	v_pk_mul_f32 v[18:19], v[32:33], v[14:15] op_sel:[1,1] op_sel_hi:[1,0] neg_lo:[1,0]
	v_add_u32_e32 v10, 0x1ff80, v13
	v_pk_fma_f32 v[14:15], v[32:33], v[14:15], v[18:19] op_sel_hi:[0,1,1]
	ds_write_b64 v10, v[14:15]
	v_mov_b32_e32 v10, v174
	v_mov_b32_e32 v13, v172
	s_waitcnt lgkmcnt(0)
	s_barrier
	v_mov_b32_e32 v14, v180
	v_xad_u32 v30, v13, 3, v10
	v_lshl_add_u32 v73, v30, 3, 0
	v_xad_u32 v30, v13, 4, v10
	v_lshl_add_u32 v72, v30, 3, 0
	v_xad_u32 v30, v13, 5, v10
	v_lshl_add_u32 v71, v30, 3, 0
	v_xad_u32 v30, v13, 6, v10
	v_lshl_add_u32 v70, v30, 3, 0
	v_xad_u32 v30, v13, 7, v10
	v_lshl_add_u32 v69, v30, 3, 0
	v_xad_u32 v30, v13, 8, v10
	v_lshl_add_u32 v30, v30, 3, 0
	v_add_u32_e32 v68, 0x800, v30
	v_xad_u32 v30, v13, 9, v10
	v_lshl_add_u32 v30, v30, 3, 0
	v_add_u32_e32 v67, 0x800, v30
	v_xad_u32 v30, v13, 10, v10
	v_lshl_add_u32 v30, v30, 3, 0
	v_add_u32_e32 v66, 0x800, v30
	v_xad_u32 v30, v13, 11, v10
	v_lshl_add_u32 v30, v30, 3, 0
	v_add_u32_e32 v18, v13, v10
	v_add_u32_e32 v65, 0x800, v30
	v_xad_u32 v30, v13, 12, v10
	v_mov_b32_e32 v15, v181
	v_lshl_add_u32 v76, v18, 3, 0
	v_lshl_add_u32 v30, v30, 3, 0
	ds_read2_b64 v[18:21], v76 offset1:16
	ds_read2_b64 v[40:43], v68 offset1:16
	v_add_u32_e32 v64, 0x800, v30
	v_xad_u32 v30, v13, 13, v10
	v_xad_u32 v22, v13, 1, v10
	v_lshl_add_u32 v30, v30, 3, 0
	v_lshl_add_u32 v75, v22, 3, 0
	v_xad_u32 v26, v13, 2, v10
	v_add_u32_e32 v63, 0x800, v30
	v_xad_u32 v30, v13, 14, v10
	v_xad_u32 v10, v13, 15, v10
	ds_read2_b64 v[22:25], v75 offset0:32 offset1:48
	ds_read2_b64 v[48:51], v67 offset0:32 offset1:48
	v_lshl_add_u32 v30, v30, 3, 0
	v_lshl_add_u32 v10, v10, 3, 0
	v_lshl_add_u32 v74, v26, 3, 0
	v_add_u32_e32 v62, 0x800, v30
	v_add_u32_e32 v13, 0x800, v10
	v_mov_b32_e32 v10, v1
	ds_read2_b64 v[26:29], v74 offset0:64 offset1:80
	ds_read2_b64 v[58:61], v73 offset0:96 offset1:112
	ds_read2_b64 v[78:81], v72 offset0:128 offset1:144
	ds_read2_b64 v[82:85], v71 offset0:160 offset1:176
	ds_read2_b64 v[86:89], v70 offset0:192 offset1:208
	ds_read2_b64 v[90:93], v69 offset0:224 offset1:240
	ds_read2_b64 v[54:57], v66 offset0:64 offset1:80
	ds_read2_b64 v[94:97], v65 offset0:96 offset1:112
	ds_read2_b64 v[98:101], v64 offset0:128 offset1:144
	ds_read2_b64 v[102:105], v63 offset0:160 offset1:176
	ds_read2_b64 v[106:109], v62 offset0:192 offset1:208
	ds_read2_b64 v[110:113], v13 offset0:224 offset1:240
	s_waitcnt lgkmcnt(14)
	v_pk_add_f32 v[114:115], v[18:19], v[40:41]
	v_pk_add_f32 v[40:41], v[18:19], v[40:41] neg_lo:[0,1] neg_hi:[0,1]
	v_pk_add_f32 v[18:19], v[20:21], v[42:43]
	v_pk_add_f32 v[20:21], v[20:21], v[42:43] neg_lo:[0,1] neg_hi:[0,1]
	v_mov_b32_e32 v30, v164
	v_mov_b32_e32 v32, v165
	v_mov_b32_e32 v34, v166
	v_mov_b32_e32 v10, v167
	v_mov_b32_e32 v38, v168
	v_mov_b32_e32 v36, v169
	v_mov_b32_e32 v46, v170
	v_mov_b32_e32 v31, v171
	v_pk_mul_f32 v[42:43], v[20:21], v[46:47] op_sel:[1,0] op_sel_hi:[0,0] neg_lo:[1,1] neg_hi:[0,1]
	s_mov_b32 s14, s95
	v_pk_fma_f32 v[44:45], v[20:21], v[30:31], v[42:43] op_sel_hi:[1,0,1]
	s_waitcnt lgkmcnt(12)
	v_pk_add_f32 v[20:21], v[22:23], v[48:49]
	v_pk_add_f32 v[22:23], v[22:23], v[48:49] neg_lo:[0,1] neg_hi:[0,1]
	s_mov_b32 s15, s94
	v_pk_mul_f32 v[42:43], v[22:23], v[36:37] op_sel:[1,0] op_sel_hi:[0,0] neg_lo:[1,1] neg_hi:[0,1]
	s_nop 0
	v_pk_fma_f32 v[48:49], v[22:23], v[32:33], v[42:43] op_sel_hi:[1,0,1]
	v_pk_add_f32 v[22:23], v[24:25], v[50:51]
	v_pk_add_f32 v[24:25], v[24:25], v[50:51] neg_lo:[0,1] neg_hi:[0,1]
	s_nop 0
	v_pk_mul_f32 v[42:43], v[24:25], v[38:39] op_sel:[1,0] op_sel_hi:[0,0] neg_lo:[1,1] neg_hi:[0,1]
	s_nop 0
	v_pk_fma_f32 v[52:53], v[24:25], v[34:35], v[42:43] op_sel_hi:[1,0,1]
	s_waitcnt lgkmcnt(5)
	v_pk_add_f32 v[24:25], v[26:27], v[54:55]
	v_pk_add_f32 v[26:27], v[26:27], v[54:55] neg_lo:[0,1] neg_hi:[0,1]
	s_nop 0
	v_pk_mul_f32 v[42:43], v[26:27], v[10:11] op_sel:[1,0] op_sel_hi:[0,0] neg_lo:[1,1] neg_hi:[0,1]
	s_nop 0
	v_pk_fma_f32 v[54:55], v[26:27], v[10:11], v[42:43] op_sel_hi:[1,0,1]
	v_pk_add_f32 v[26:27], v[28:29], v[56:57]
	v_pk_add_f32 v[28:29], v[28:29], v[56:57] neg_lo:[0,1] neg_hi:[0,1]
	s_nop 0
	v_pk_mul_f32 v[42:43], v[28:29], v[38:39] op_sel_hi:[1,0]
	s_nop 0
	v_pk_fma_f32 v[56:57], v[28:29], v[34:35], v[42:43] op_sel:[1,0,0] op_sel_hi:[0,0,1] neg_lo:[1,1,0] neg_hi:[0,1,0]
	s_waitcnt lgkmcnt(4)
	v_pk_add_f32 v[42:43], v[58:59], v[94:95] neg_lo:[0,1] neg_hi:[0,1]
	v_pk_add_f32 v[28:29], v[58:59], v[94:95]
	v_pk_mul_f32 v[50:51], v[42:43], v[36:37] op_sel_hi:[1,0]
	s_nop 0
	v_pk_fma_f32 v[58:59], v[42:43], v[32:33], v[50:51] op_sel:[1,0,0] op_sel_hi:[0,0,1] neg_lo:[1,1,0] neg_hi:[0,1,0]
	v_pk_add_f32 v[50:51], v[60:61], v[96:97] neg_lo:[0,1] neg_hi:[0,1]
	v_pk_add_f32 v[42:43], v[60:61], v[96:97]
	v_pk_mul_f32 v[60:61], v[50:51], v[46:47] op_sel_hi:[1,0]
	v_xor_b32_e32 v94, 0x80000000, v51
	v_mov_b32_e32 v95, v50
	s_waitcnt lgkmcnt(3)
	v_pk_add_f32 v[50:51], v[78:79], v[98:99]
	v_pk_add_f32 v[78:79], v[78:79], v[98:99] neg_lo:[0,1] neg_hi:[0,1]
	v_pk_fma_f32 v[60:61], v[94:95], v[30:31], v[60:61] op_sel_hi:[1,0,1] neg_lo:[0,1,0] neg_hi:[0,1,0]
	v_xor_b32_e32 v95, 0x80000000, v78
	v_mov_b32_e32 v94, v79
	v_pk_add_f32 v[78:79], v[80:81], v[100:101]
	v_pk_add_f32 v[80:81], v[80:81], v[100:101] neg_lo:[0,1] neg_hi:[0,1]
	s_nop 0
	v_pk_mul_f32 v[96:97], v[80:81], v[46:47] op_sel_hi:[1,0] neg_lo:[0,1] neg_hi:[0,1]
	s_nop 0
	v_pk_fma_f32 v[80:81], v[80:81], v[30:31], v[96:97] op_sel:[1,0,0] op_sel_hi:[0,0,1] neg_lo:[1,1,0] neg_hi:[0,1,0]
	s_waitcnt lgkmcnt(2)
	v_pk_add_f32 v[96:97], v[82:83], v[102:103]
	v_pk_add_f32 v[82:83], v[82:83], v[102:103] neg_lo:[0,1] neg_hi:[0,1]
	s_nop 0
	v_pk_mul_f32 v[98:99], v[82:83], v[36:37] op_sel_hi:[1,0] neg_lo:[0,1] neg_hi:[0,1]
	s_nop 0
	v_pk_fma_f32 v[82:83], v[82:83], v[32:33], v[98:99] op_sel:[1,0,0] op_sel_hi:[0,0,1] neg_lo:[1,1,0] neg_hi:[0,1,0]
	v_pk_add_f32 v[98:99], v[84:85], v[104:105]
	v_pk_add_f32 v[84:85], v[84:85], v[104:105] neg_lo:[0,1] neg_hi:[0,1]
	s_nop 0
	v_pk_mul_f32 v[100:101], v[84:85], v[38:39] op_sel_hi:[1,0] neg_lo:[0,1] neg_hi:[0,1]
	s_nop 0
	v_pk_fma_f32 v[84:85], v[84:85], v[34:35], v[100:101] op_sel:[1,0,0] op_sel_hi:[0,0,1] neg_lo:[1,1,0] neg_hi:[0,1,0]
	s_waitcnt lgkmcnt(1)
	v_pk_add_f32 v[100:101], v[86:87], v[106:107]
	v_pk_add_f32 v[86:87], v[86:87], v[106:107] neg_lo:[0,1] neg_hi:[0,1]
	s_nop 0
	v_pk_mul_f32 v[102:103], v[86:87], v[10:11] op_sel:[1,0] op_sel_hi:[0,0] neg_lo:[1,1] neg_hi:[0,1]
	s_nop 0
	v_pk_fma_f32 v[86:87], v[86:87], v[10:11], v[102:103] op_sel_hi:[1,0,1] neg_lo:[0,1,0] neg_hi:[0,1,0]
	v_pk_add_f32 v[102:103], v[88:89], v[108:109]
	v_pk_add_f32 v[88:89], v[88:89], v[108:109] neg_lo:[0,1] neg_hi:[0,1]
	s_nop 0
	v_pk_mul_f32 v[38:39], v[88:89], v[38:39] op_sel:[1,0] op_sel_hi:[0,0] neg_lo:[1,1] neg_hi:[0,1]
	s_nop 0
	v_pk_fma_f32 v[88:89], v[88:89], v[34:35], v[38:39] op_sel_hi:[1,0,1] neg_lo:[0,1,0] neg_hi:[0,1,0]
	s_waitcnt lgkmcnt(0)
	v_pk_add_f32 v[38:39], v[90:91], v[110:111] neg_lo:[0,1] neg_hi:[0,1]
	v_pk_add_f32 v[34:35], v[90:91], v[110:111]
	v_pk_mul_f32 v[90:91], v[38:39], v[36:37] op_sel:[1,0] op_sel_hi:[0,0] neg_lo:[1,1] neg_hi:[0,1]
	s_nop 0
	v_pk_fma_f32 v[90:91], v[38:39], v[32:33], v[90:91] op_sel_hi:[1,0,1] neg_lo:[0,1,0] neg_hi:[0,1,0]
	v_pk_add_f32 v[38:39], v[92:93], v[112:113]
	v_pk_add_f32 v[92:93], v[92:93], v[112:113] neg_lo:[0,1] neg_hi:[0,1]
	s_nop 0
	v_pk_mul_f32 v[46:47], v[92:93], v[46:47] op_sel:[1,0] op_sel_hi:[0,0] neg_lo:[1,1] neg_hi:[0,1]
	s_nop 0
	v_pk_fma_f32 v[92:93], v[92:93], v[30:31], v[46:47] op_sel_hi:[1,0,1] neg_lo:[0,1,0] neg_hi:[0,1,0]
	v_pk_add_f32 v[46:47], v[18:19], v[78:79]
	v_pk_add_f32 v[18:19], v[18:19], v[78:79] neg_lo:[0,1] neg_hi:[0,1]
	v_pk_add_f32 v[30:31], v[114:115], v[50:51]
	v_pk_mul_f32 v[78:79], v[18:19], v[36:37] op_sel:[1,0] op_sel_hi:[0,0] neg_lo:[1,1] neg_hi:[0,1]
	v_pk_add_f32 v[50:51], v[114:115], v[50:51] neg_lo:[0,1] neg_hi:[0,1]
	v_pk_fma_f32 v[78:79], v[18:19], v[32:33], v[78:79] op_sel_hi:[1,0,1]
	v_pk_add_f32 v[18:19], v[20:21], v[96:97]
	v_pk_add_f32 v[20:21], v[20:21], v[96:97] neg_lo:[0,1] neg_hi:[0,1]
	s_nop 0
	v_pk_mul_f32 v[96:97], v[20:21], v[10:11] op_sel:[1,0] op_sel_hi:[0,0] neg_lo:[1,1] neg_hi:[0,1]
	s_nop 0
	v_pk_fma_f32 v[20:21], v[20:21], v[10:11], v[96:97] op_sel_hi:[1,0,1]
	v_pk_add_f32 v[96:97], v[22:23], v[98:99]
	v_pk_add_f32 v[22:23], v[22:23], v[98:99] neg_lo:[0,1] neg_hi:[0,1]
	s_nop 0
	v_pk_mul_f32 v[98:99], v[22:23], v[36:37] op_sel_hi:[1,0]
	v_xor_b32_e32 v104, 0x80000000, v23
	v_mov_b32_e32 v105, v22
	v_pk_add_f32 v[22:23], v[24:25], v[100:101]
	v_pk_add_f32 v[24:25], v[24:25], v[100:101] neg_lo:[0,1] neg_hi:[0,1]
	v_pk_fma_f32 v[98:99], v[104:105], v[32:33], v[98:99] op_sel_hi:[1,0,1] neg_lo:[0,1,0] neg_hi:[0,1,0]
	v_xor_b32_e32 v101, 0x80000000, v24
	v_mov_b32_e32 v100, v25
	v_pk_add_f32 v[24:25], v[26:27], v[102:103]
	v_pk_add_f32 v[26:27], v[26:27], v[102:103] neg_lo:[0,1] neg_hi:[0,1]
	s_nop 0
	v_pk_mul_f32 v[102:103], v[26:27], v[36:37] op_sel_hi:[1,0] neg_lo:[0,1] neg_hi:[0,1]
	v_xor_b32_e32 v104, 0x80000000, v27
	v_mov_b32_e32 v105, v26
	v_pk_add_f32 v[26:27], v[28:29], v[34:35]
	v_pk_add_f32 v[28:29], v[28:29], v[34:35] neg_lo:[0,1] neg_hi:[0,1]
	v_pk_fma_f32 v[102:103], v[104:105], v[32:33], v[102:103] op_sel_hi:[1,0,1] neg_lo:[0,1,0] neg_hi:[0,1,0]
	v_pk_mul_f32 v[34:35], v[28:29], v[10:11] op_sel:[1,0] op_sel_hi:[0,0] neg_lo:[1,1] neg_hi:[0,1]
	v_pk_add_f32 v[104:105], v[30:31], v[22:23] neg_lo:[0,1] neg_hi:[0,1]
	v_pk_fma_f32 v[28:29], v[28:29], v[10:11], v[34:35] op_sel_hi:[1,0,1] neg_lo:[0,1,0] neg_hi:[0,1,0]
	v_pk_add_f32 v[34:35], v[42:43], v[38:39]
	v_pk_add_f32 v[38:39], v[42:43], v[38:39] neg_lo:[0,1] neg_hi:[0,1]
	s_nop 0
	v_pk_mul_f32 v[42:43], v[38:39], v[36:37] op_sel:[1,0] op_sel_hi:[0,0] neg_lo:[1,1] neg_hi:[0,1]
	s_nop 0
	v_pk_fma_f32 v[42:43], v[38:39], v[32:33], v[42:43] op_sel_hi:[1,0,1] neg_lo:[0,1,0] neg_hi:[0,1,0]
	v_pk_add_f32 v[38:39], v[30:31], v[22:23]
	v_pk_add_f32 v[22:23], v[46:47], v[24:25]
	v_pk_add_f32 v[24:25], v[46:47], v[24:25] neg_lo:[0,1] neg_hi:[0,1]
	s_nop 0
	v_pk_mul_f32 v[30:31], v[24:25], v[10:11] op_sel:[1,0] op_sel_hi:[0,0] neg_lo:[1,1] neg_hi:[0,1]
	s_nop 0
	v_pk_fma_f32 v[24:25], v[24:25], v[10:11], v[30:31] op_sel_hi:[1,0,1]
	v_pk_add_f32 v[30:31], v[18:19], v[26:27]
	v_pk_add_f32 v[18:19], v[18:19], v[26:27] neg_lo:[0,1] neg_hi:[0,1]
	s_nop 0
	v_xor_b32_e32 v27, 0x80000000, v18
	v_mov_b32_e32 v26, v19
	v_pk_add_f32 v[18:19], v[96:97], v[34:35]
	v_pk_add_f32 v[34:35], v[96:97], v[34:35] neg_lo:[0,1] neg_hi:[0,1]
	s_nop 0
	v_pk_mul_f32 v[46:47], v[34:35], v[10:11] op_sel:[1,0] op_sel_hi:[0,0] neg_lo:[1,1] neg_hi:[0,1]
	s_nop 0
	v_pk_fma_f32 v[34:35], v[34:35], v[10:11], v[46:47] op_sel_hi:[1,0,1] neg_lo:[0,1,0] neg_hi:[0,1,0]
	v_pk_add_f32 v[46:47], v[38:39], v[30:31]
	v_pk_add_f32 v[38:39], v[38:39], v[30:31] neg_lo:[0,1] neg_hi:[0,1]
	v_pk_add_f32 v[30:31], v[22:23], v[18:19]
	v_pk_add_f32 v[18:19], v[22:23], v[18:19] neg_lo:[0,1] neg_hi:[0,1]
	v_pk_add_f32 v[96:97], v[46:47], v[30:31]
	v_xor_b32_e32 v23, 0x80000000, v18
	v_mov_b32_e32 v22, v19
	v_pk_add_f32 v[18:19], v[104:105], v[26:27]
	v_pk_add_f32 v[104:105], v[104:105], v[26:27] neg_lo:[0,1] neg_hi:[0,1]
	v_pk_add_f32 v[26:27], v[24:25], v[34:35]
	v_pk_add_f32 v[24:25], v[24:25], v[34:35] neg_lo:[0,1] neg_hi:[0,1]
	v_pk_add_f32 v[30:31], v[46:47], v[30:31] neg_lo:[0,1] neg_hi:[0,1]
	v_xor_b32_e32 v35, 0x80000000, v24
	v_mov_b32_e32 v34, v25
	v_pk_add_f32 v[24:25], v[50:51], v[100:101]
	v_pk_add_f32 v[100:101], v[50:51], v[100:101] neg_lo:[0,1] neg_hi:[0,1]
	v_pk_add_f32 v[50:51], v[78:79], v[102:103] neg_lo:[0,1] neg_hi:[0,1]
	v_pk_add_f32 v[46:47], v[38:39], v[22:23]
	v_pk_add_f32 v[22:23], v[38:39], v[22:23] neg_lo:[0,1] neg_hi:[0,1]
	v_pk_add_f32 v[106:107], v[18:19], v[26:27]
	v_pk_add_f32 v[26:27], v[18:19], v[26:27] neg_lo:[0,1] neg_hi:[0,1]
	v_pk_add_f32 v[38:39], v[104:105], v[34:35]
	v_pk_add_f32 v[18:19], v[104:105], v[34:35] neg_lo:[0,1] neg_hi:[0,1]
	v_pk_add_f32 v[34:35], v[78:79], v[102:103]
	v_pk_mul_f32 v[78:79], v[10:11], v[50:51] op_sel:[0,1] op_sel_hi:[0,0] neg_lo:[1,1] neg_hi:[1,0]
	v_pk_fma_f32 v[78:79], v[10:11], v[50:51], v[78:79] op_sel_hi:[0,1,1]
	v_pk_add_f32 v[50:51], v[20:21], v[28:29]
	v_pk_add_f32 v[20:21], v[20:21], v[28:29] neg_lo:[0,1] neg_hi:[0,1]
	s_nop 0
	v_xor_b32_e32 v29, 0x80000000, v20
	v_mov_b32_e32 v28, v21
	v_pk_add_f32 v[20:21], v[98:99], v[42:43]
	v_pk_add_f32 v[42:43], v[98:99], v[42:43] neg_lo:[0,1] neg_hi:[0,1]
	s_nop 0
	v_pk_mul_f32 v[98:99], v[10:11], v[42:43] op_sel:[0,1] op_sel_hi:[0,0] neg_lo:[1,1] neg_hi:[1,0]
	v_pk_fma_f32 v[42:43], v[10:11], v[42:43], v[98:99] op_sel_hi:[0,1,1] neg_lo:[1,0,0] neg_hi:[1,0,0]
	v_pk_add_f32 v[98:99], v[24:25], v[50:51]
	v_pk_add_f32 v[24:25], v[24:25], v[50:51] neg_lo:[0,1] neg_hi:[0,1]
	v_pk_add_f32 v[50:51], v[34:35], v[20:21]
	v_pk_add_f32 v[20:21], v[34:35], v[20:21] neg_lo:[0,1] neg_hi:[0,1]
	v_pk_add_f32 v[104:105], v[98:99], v[50:51]
	v_xor_b32_e32 v103, 0x80000000, v20
	v_mov_b32_e32 v102, v21
	v_pk_add_f32 v[34:35], v[98:99], v[50:51] neg_lo:[0,1] neg_hi:[0,1]
	v_pk_add_f32 v[20:21], v[100:101], v[28:29]
	v_pk_add_f32 v[98:99], v[100:101], v[28:29] neg_lo:[0,1] neg_hi:[0,1]
	v_pk_add_f32 v[28:29], v[78:79], v[42:43]
	v_pk_add_f32 v[42:43], v[78:79], v[42:43] neg_lo:[0,1] neg_hi:[0,1]
	v_pk_add_f32 v[100:101], v[20:21], v[28:29]
	v_xor_b32_e32 v79, 0x80000000, v42
	v_mov_b32_e32 v78, v43
	v_pk_add_f32 v[28:29], v[20:21], v[28:29] neg_lo:[0,1] neg_hi:[0,1]
	v_pk_add_f32 v[42:43], v[98:99], v[78:79]
	v_pk_add_f32 v[20:21], v[98:99], v[78:79] neg_lo:[0,1] neg_hi:[0,1]
	v_pk_add_f32 v[78:79], v[40:41], v[94:95]
	v_pk_add_f32 v[94:95], v[40:41], v[94:95] neg_lo:[0,1] neg_hi:[0,1]
	v_pk_add_f32 v[40:41], v[44:45], v[80:81]
	v_pk_add_f32 v[44:45], v[44:45], v[80:81] neg_lo:[0,1] neg_hi:[0,1]
	v_pk_add_f32 v[50:51], v[24:25], v[102:103]
	v_pk_mul_f32 v[80:81], v[36:37], v[44:45] op_sel:[0,1] op_sel_hi:[0,0] neg_lo:[1,1] neg_hi:[1,0]
	v_pk_fma_f32 v[44:45], v[32:33], v[44:45], v[80:81] op_sel_hi:[0,1,1]
	v_pk_add_f32 v[80:81], v[48:49], v[82:83]
	v_pk_add_f32 v[48:49], v[48:49], v[82:83] neg_lo:[0,1] neg_hi:[0,1]
	v_pk_add_f32 v[24:25], v[24:25], v[102:103] neg_lo:[0,1] neg_hi:[0,1]
	v_pk_mul_f32 v[82:83], v[10:11], v[48:49] op_sel:[0,1] op_sel_hi:[0,0] neg_lo:[1,1] neg_hi:[1,0]
	v_pk_fma_f32 v[82:83], v[10:11], v[48:49], v[82:83] op_sel_hi:[0,1,1]
	v_pk_add_f32 v[48:49], v[52:53], v[84:85]
	v_pk_add_f32 v[52:53], v[52:53], v[84:85] neg_lo:[0,1] neg_hi:[0,1]
	s_nop 0
	v_pk_mul_f32 v[84:85], v[32:33], v[52:53] op_sel:[0,1] op_sel_hi:[0,0] neg_lo:[1,1] neg_hi:[1,0]
	v_pk_fma_f32 v[52:53], v[36:37], v[52:53], v[84:85] op_sel_hi:[0,1,1]
	v_pk_add_f32 v[84:85], v[54:55], v[86:87]
	v_pk_add_f32 v[54:55], v[54:55], v[86:87] neg_lo:[0,1] neg_hi:[0,1]
	s_nop 0
	v_xor_b32_e32 v87, 0x80000000, v54
	v_mov_b32_e32 v86, v55
	v_pk_add_f32 v[54:55], v[56:57], v[88:89]
	v_pk_add_f32 v[56:57], v[56:57], v[88:89] neg_lo:[0,1] neg_hi:[0,1]
	s_nop 0
	v_pk_mul_f32 v[88:89], v[32:33], v[56:57] op_sel:[0,1] op_sel_hi:[0,0] neg_lo:[1,1] neg_hi:[1,0]
	v_pk_fma_f32 v[56:57], v[36:37], v[56:57], v[88:89] op_sel_hi:[0,1,1] neg_lo:[1,0,0] neg_hi:[1,0,0]
	v_pk_add_f32 v[88:89], v[58:59], v[90:91]
	v_pk_add_f32 v[58:59], v[58:59], v[90:91] neg_lo:[0,1] neg_hi:[0,1]
	s_nop 0
	v_pk_mul_f32 v[90:91], v[10:11], v[58:59] op_sel:[0,1] op_sel_hi:[0,0] neg_lo:[1,1] neg_hi:[1,0]
	v_pk_fma_f32 v[58:59], v[10:11], v[58:59], v[90:91] op_sel_hi:[0,1,1] neg_lo:[1,0,0] neg_hi:[1,0,0]
	v_pk_add_f32 v[90:91], v[60:61], v[92:93]
	v_pk_add_f32 v[60:61], v[60:61], v[92:93] neg_lo:[0,1] neg_hi:[0,1]
	s_nop 0
	v_pk_mul_f32 v[36:37], v[36:37], v[60:61] op_sel:[0,1] op_sel_hi:[0,0] neg_lo:[1,1] neg_hi:[1,0]
	v_pk_fma_f32 v[36:37], v[32:33], v[60:61], v[36:37] op_sel_hi:[0,1,1] neg_lo:[1,0,0] neg_hi:[1,0,0]
	v_pk_add_f32 v[32:33], v[78:79], v[84:85]
	v_pk_add_f32 v[60:61], v[78:79], v[84:85] neg_lo:[0,1] neg_hi:[0,1]
	v_pk_add_f32 v[78:79], v[54:55], v[40:41]
	v_pk_add_f32 v[40:41], v[40:41], v[54:55] neg_lo:[0,1] neg_hi:[0,1]
	s_nop 0
	v_pk_mul_f32 v[54:55], v[10:11], v[40:41] op_sel:[0,1] op_sel_hi:[0,0] neg_lo:[1,1] neg_hi:[1,0]
	v_pk_fma_f32 v[54:55], v[10:11], v[40:41], v[54:55] op_sel_hi:[0,1,1]
	v_pk_add_f32 v[40:41], v[80:81], v[88:89]
	v_pk_add_f32 v[80:81], v[80:81], v[88:89] neg_lo:[0,1] neg_hi:[0,1]
	s_nop 0
	v_xor_b32_e32 v85, 0x80000000, v80
	v_mov_b32_e32 v84, v81
	v_pk_add_f32 v[80:81], v[48:49], v[90:91]
	v_pk_add_f32 v[48:49], v[48:49], v[90:91] neg_lo:[0,1] neg_hi:[0,1]
	v_pk_add_f32 v[90:91], v[78:79], v[80:81]
	v_pk_mul_f32 v[88:89], v[10:11], v[48:49] op_sel:[0,1] op_sel_hi:[0,0] neg_lo:[1,1] neg_hi:[1,0]
	v_pk_fma_f32 v[48:49], v[10:11], v[48:49], v[88:89] op_sel_hi:[0,1,1] neg_lo:[1,0,0] neg_hi:[1,0,0]
	v_pk_add_f32 v[88:89], v[32:33], v[40:41]
	v_pk_add_f32 v[32:33], v[32:33], v[40:41] neg_lo:[0,1] neg_hi:[0,1]
	v_pk_add_f32 v[40:41], v[78:79], v[80:81] neg_lo:[0,1] neg_hi:[0,1]
	v_pk_add_f32 v[80:81], v[88:89], v[90:91] neg_lo:[0,1] neg_hi:[0,1]
	v_pk_add_f32 v[92:93], v[32:33], v[40:41] op_sel:[0,1] op_sel_hi:[1,0] neg_hi:[0,1]
	v_pk_add_f32 v[40:41], v[32:33], v[40:41] op_sel:[0,1] op_sel_hi:[1,0] neg_lo:[0,1]
	v_pk_add_f32 v[78:79], v[54:55], v[48:49]
	v_pk_add_f32 v[48:49], v[54:55], v[48:49] neg_lo:[0,1] neg_hi:[0,1]
	v_pk_add_f32 v[32:33], v[60:61], v[84:85]
	v_pk_add_f32 v[60:61], v[60:61], v[84:85] neg_lo:[0,1] neg_hi:[0,1]
	v_xor_b32_e32 v55, 0x80000000, v48
	v_mov_b32_e32 v54, v49
	v_pk_add_f32 v[84:85], v[32:33], v[78:79]
	v_pk_add_f32 v[48:49], v[32:33], v[78:79] neg_lo:[0,1] neg_hi:[0,1]
	v_pk_add_f32 v[78:79], v[60:61], v[54:55]
	v_pk_add_f32 v[32:33], v[60:61], v[54:55] neg_lo:[0,1] neg_hi:[0,1]
	v_pk_add_f32 v[54:55], v[94:95], v[86:87]
	v_pk_add_f32 v[60:61], v[94:95], v[86:87] neg_lo:[0,1] neg_hi:[0,1]
	v_pk_add_f32 v[86:87], v[56:57], v[44:45]
	v_pk_add_f32 v[44:45], v[44:45], v[56:57] neg_lo:[0,1] neg_hi:[0,1]
	v_pk_add_f32 v[88:89], v[88:89], v[90:91]
	v_pk_mul_f32 v[56:57], v[10:11], v[44:45] op_sel:[0,1] op_sel_hi:[0,0] neg_lo:[1,1] neg_hi:[1,0]
	v_pk_fma_f32 v[56:57], v[10:11], v[44:45], v[56:57] op_sel_hi:[0,1,1]
	v_pk_add_f32 v[44:45], v[82:83], v[58:59]
	v_pk_add_f32 v[58:59], v[82:83], v[58:59] neg_lo:[0,1] neg_hi:[0,1]
	s_nop 0
	v_xor_b32_e32 v83, 0x80000000, v58
	v_mov_b32_e32 v82, v59
	v_pk_add_f32 v[58:59], v[52:53], v[36:37]
	v_pk_add_f32 v[36:37], v[52:53], v[36:37] neg_lo:[0,1] neg_hi:[0,1]
	s_nop 0
	v_pk_mul_f32 v[52:53], v[10:11], v[36:37] op_sel:[0,1] op_sel_hi:[0,0] neg_lo:[1,1] neg_hi:[1,0]
	v_pk_fma_f32 v[36:37], v[10:11], v[36:37], v[52:53] op_sel_hi:[0,1,1] neg_lo:[1,0,0] neg_hi:[1,0,0]
	v_pk_add_f32 v[52:53], v[54:55], v[44:45]
	v_pk_add_f32 v[44:45], v[54:55], v[44:45] neg_lo:[0,1] neg_hi:[0,1]
	v_pk_add_f32 v[54:55], v[86:87], v[58:59]
	v_pk_add_f32 v[58:59], v[86:87], v[58:59] neg_lo:[0,1] neg_hi:[0,1]
	s_nop 0
	v_xor_b32_e32 v87, 0x80000000, v58
	v_mov_b32_e32 v86, v59
	v_pk_add_f32 v[58:59], v[52:53], v[54:55]
	v_pk_add_f32 v[54:55], v[52:53], v[54:55] neg_lo:[0,1] neg_hi:[0,1]
	v_pk_add_f32 v[52:53], v[60:61], v[82:83]
	v_pk_add_f32 v[60:61], v[60:61], v[82:83] neg_lo:[0,1] neg_hi:[0,1]
	v_pk_add_f32 v[82:83], v[56:57], v[36:37]
	v_pk_add_f32 v[36:37], v[56:57], v[36:37] neg_lo:[0,1] neg_hi:[0,1]
	v_pk_add_f32 v[94:95], v[44:45], v[86:87]
	v_pk_add_f32 v[44:45], v[44:45], v[86:87] neg_lo:[0,1] neg_hi:[0,1]
	v_pk_add_f32 v[86:87], v[52:53], v[82:83]
	v_pk_add_f32 v[52:53], v[52:53], v[82:83] neg_lo:[0,1] neg_hi:[0,1]
	v_pk_add_f32 v[82:83], v[60:61], v[36:37] op_sel:[0,1] op_sel_hi:[1,0] neg_hi:[0,1]
	v_pk_add_f32 v[36:37], v[60:61], v[36:37] op_sel:[0,1] op_sel_hi:[1,0] neg_lo:[0,1]
	v_pk_fma_f32 v[60:61], v[14:15], s[90:91], v[14:15] op_sel:[1,0,0] op_sel_hi:[0,1,1]
	v_pk_mul_f32 v[56:57], v[96:97], s[14:15] op_sel:[1,0] neg_lo:[1,0]
	v_pk_mul_f32 v[90:91], v[60:61], v[88:89] op_sel:[1,1] op_sel_hi:[0,1] neg_lo:[0,1]
	v_pk_fma_f32 v[56:57], v[96:97], s[94:95], v[56:57] op_sel_hi:[0,1,1]
	v_pk_fma_f32 v[88:89], v[60:61], v[88:89], v[90:91] op_sel_hi:[1,0,1]
	ds_write2_b64 v76, v[56:57], v[88:89] offset1:16
	v_pk_mul_f32 v[56:57], v[14:15], v[60:61] op_sel:[1,1] op_sel_hi:[0,1] neg_lo:[0,1]
	v_pk_fma_f32 v[56:57], v[14:15], v[60:61], v[56:57] op_sel_hi:[1,0,1]
	s_nop 0
	v_pk_mul_f32 v[60:61], v[56:57], v[104:105] op_sel:[1,1] op_sel_hi:[0,1] neg_lo:[0,1]
	v_pk_mul_f32 v[76:77], v[14:15], v[56:57] op_sel:[1,1] op_sel_hi:[0,1] neg_lo:[0,1]
	v_pk_fma_f32 v[60:61], v[56:57], v[104:105], v[60:61] op_sel_hi:[1,0,1]
	v_pk_fma_f32 v[56:57], v[14:15], v[56:57], v[76:77] op_sel_hi:[1,0,1]
	s_nop 0
	v_pk_mul_f32 v[76:77], v[56:57], v[58:59] op_sel:[1,1] op_sel_hi:[0,1] neg_lo:[0,1]
	v_pk_fma_f32 v[58:59], v[56:57], v[58:59], v[76:77] op_sel_hi:[1,0,1]
	ds_write2_b64 v75, v[60:61], v[58:59] offset0:32 offset1:48
	v_pk_mul_f32 v[58:59], v[14:15], v[56:57] op_sel:[1,1] op_sel_hi:[0,1] neg_lo:[0,1]
	v_pk_fma_f32 v[56:57], v[14:15], v[56:57], v[58:59] op_sel_hi:[1,0,1]
	s_nop 0
	v_pk_mul_f32 v[58:59], v[56:57], v[106:107] op_sel:[1,1] op_sel_hi:[0,1] neg_lo:[0,1]
	v_pk_mul_f32 v[60:61], v[14:15], v[56:57] op_sel:[1,1] op_sel_hi:[0,1] neg_lo:[0,1]
	v_pk_fma_f32 v[58:59], v[56:57], v[106:107], v[58:59] op_sel_hi:[1,0,1]
	v_pk_fma_f32 v[56:57], v[14:15], v[56:57], v[60:61] op_sel_hi:[1,0,1]
	s_nop 0
	v_pk_mul_f32 v[60:61], v[56:57], v[84:85] op_sel:[1,1] op_sel_hi:[0,1] neg_lo:[0,1]
	v_pk_fma_f32 v[60:61], v[56:57], v[84:85], v[60:61] op_sel_hi:[1,0,1]
	ds_write2_b64 v74, v[58:59], v[60:61] offset0:64 offset1:80
	v_pk_mul_f32 v[58:59], v[14:15], v[56:57] op_sel:[1,1] op_sel_hi:[0,1] neg_lo:[0,1]
	v_pk_fma_f32 v[56:57], v[14:15], v[56:57], v[58:59] op_sel_hi:[1,0,1]
	s_nop 0
	v_pk_mul_f32 v[58:59], v[56:57], v[100:101] op_sel:[1,1] op_sel_hi:[0,1] neg_lo:[0,1]
	v_pk_mul_f32 v[60:61], v[14:15], v[56:57] op_sel:[1,1] op_sel_hi:[0,1] neg_lo:[0,1]
	v_pk_fma_f32 v[58:59], v[56:57], v[100:101], v[58:59] op_sel_hi:[1,0,1]
	v_pk_fma_f32 v[56:57], v[14:15], v[56:57], v[60:61] op_sel_hi:[1,0,1]
	s_nop 0
	v_pk_mul_f32 v[60:61], v[56:57], v[86:87] op_sel:[1,1] op_sel_hi:[0,1] neg_lo:[0,1]
	v_pk_fma_f32 v[60:61], v[56:57], v[86:87], v[60:61] op_sel_hi:[1,0,1]
	ds_write2_b64 v73, v[58:59], v[60:61] offset0:96 offset1:112
	v_pk_mul_f32 v[58:59], v[14:15], v[56:57] op_sel:[1,1] op_sel_hi:[0,1] neg_lo:[0,1]
	v_pk_fma_f32 v[56:57], v[14:15], v[56:57], v[58:59] op_sel_hi:[1,0,1]
	s_nop 0
	v_pk_mul_f32 v[58:59], v[56:57], v[46:47] op_sel:[1,1] op_sel_hi:[0,1] neg_lo:[0,1]
	v_pk_fma_f32 v[46:47], v[56:57], v[46:47], v[58:59] op_sel_hi:[1,0,1]
	v_pk_mul_f32 v[58:59], v[14:15], v[56:57] op_sel:[1,1] op_sel_hi:[0,1] neg_lo:[0,1]
	v_pk_fma_f32 v[56:57], v[14:15], v[56:57], v[58:59] op_sel_hi:[1,0,1]
	s_nop 0
	v_pk_mul_f32 v[58:59], v[56:57], v[92:93] op_sel:[1,1] op_sel_hi:[0,1] neg_lo:[0,1]
	v_pk_fma_f32 v[58:59], v[56:57], v[92:93], v[58:59] op_sel_hi:[1,0,1]
	ds_write2_b64 v72, v[46:47], v[58:59] offset0:128 offset1:144
	v_pk_mul_f32 v[46:47], v[14:15], v[56:57] op_sel:[1,1] op_sel_hi:[0,1] neg_lo:[0,1]
	v_pk_fma_f32 v[46:47], v[14:15], v[56:57], v[46:47] op_sel_hi:[1,0,1]
	s_nop 0
	v_pk_mul_f32 v[56:57], v[46:47], v[50:51] op_sel:[1,1] op_sel_hi:[0,1] neg_lo:[0,1]
	v_pk_fma_f32 v[50:51], v[46:47], v[50:51], v[56:57] op_sel_hi:[1,0,1]
	v_pk_mul_f32 v[56:57], v[14:15], v[46:47] op_sel:[1,1] op_sel_hi:[0,1] neg_lo:[0,1]
	v_pk_fma_f32 v[46:47], v[14:15], v[46:47], v[56:57] op_sel_hi:[1,0,1]
	s_nop 0
	v_pk_mul_f32 v[56:57], v[46:47], v[94:95] op_sel:[1,1] op_sel_hi:[0,1] neg_lo:[0,1]
	v_pk_fma_f32 v[56:57], v[46:47], v[94:95], v[56:57] op_sel_hi:[1,0,1]
	ds_write2_b64 v71, v[50:51], v[56:57] offset0:160 offset1:176
	v_pk_mul_f32 v[50:51], v[14:15], v[46:47] op_sel:[1,1] op_sel_hi:[0,1] neg_lo:[0,1]
	v_pk_fma_f32 v[46:47], v[14:15], v[46:47], v[50:51] op_sel_hi:[1,0,1]
	s_nop 0
	v_pk_mul_f32 v[50:51], v[38:39], v[46:47] op_sel:[1,1] op_sel_hi:[1,0] neg_lo:[1,0]
	s_nop 0
	v_pk_fma_f32 v[38:39], v[38:39], v[46:47], v[50:51] op_sel_hi:[0,1,1]
	v_pk_mul_f32 v[50:51], v[14:15], v[46:47] op_sel:[1,1] op_sel_hi:[0,1] neg_lo:[0,1]
	v_pk_fma_f32 v[46:47], v[14:15], v[46:47], v[50:51] op_sel_hi:[1,0,1]
	s_nop 0
	v_pk_mul_f32 v[50:51], v[46:47], v[78:79] op_sel:[1,1] op_sel_hi:[0,1] neg_lo:[0,1]
	v_pk_fma_f32 v[50:51], v[46:47], v[78:79], v[50:51] op_sel_hi:[1,0,1]
	ds_write2_b64 v70, v[38:39], v[50:51] offset0:192 offset1:208
	v_pk_mul_f32 v[38:39], v[14:15], v[46:47] op_sel:[1,1] op_sel_hi:[0,1] neg_lo:[0,1]
	v_pk_fma_f32 v[38:39], v[14:15], v[46:47], v[38:39] op_sel_hi:[1,0,1]
	s_nop 0
	v_pk_mul_f32 v[46:47], v[42:43], v[38:39] op_sel:[1,1] op_sel_hi:[1,0] neg_lo:[1,0]
	s_nop 0
	v_pk_fma_f32 v[42:43], v[42:43], v[38:39], v[46:47] op_sel_hi:[0,1,1]
	v_pk_mul_f32 v[46:47], v[14:15], v[38:39] op_sel:[1,1] op_sel_hi:[0,1] neg_lo:[0,1]
	v_pk_fma_f32 v[38:39], v[14:15], v[38:39], v[46:47] op_sel_hi:[1,0,1]
	s_nop 0
	v_pk_mul_f32 v[46:47], v[38:39], v[82:83] op_sel:[1,1] op_sel_hi:[0,1] neg_lo:[0,1]
	v_pk_fma_f32 v[46:47], v[38:39], v[82:83], v[46:47] op_sel_hi:[1,0,1]
	ds_write2_b64 v69, v[42:43], v[46:47] offset0:224 offset1:240
	v_pk_mul_f32 v[42:43], v[14:15], v[38:39] op_sel:[1,1] op_sel_hi:[0,1] neg_lo:[0,1]
	v_pk_fma_f32 v[38:39], v[14:15], v[38:39], v[42:43] op_sel_hi:[1,0,1]
	s_nop 0
	v_pk_mul_f32 v[42:43], v[30:31], v[38:39] op_sel:[1,1] op_sel_hi:[1,0] neg_lo:[1,0]
	s_nop 0
	v_pk_fma_f32 v[30:31], v[30:31], v[38:39], v[42:43] op_sel_hi:[0,1,1]
	v_pk_mul_f32 v[42:43], v[14:15], v[38:39] op_sel:[1,1] op_sel_hi:[0,1] neg_lo:[0,1]
	v_pk_fma_f32 v[38:39], v[14:15], v[38:39], v[42:43] op_sel_hi:[1,0,1]
	s_nop 0
	v_pk_mul_f32 v[42:43], v[80:81], v[38:39] op_sel:[1,1] op_sel_hi:[1,0] neg_lo:[1,0]
	s_nop 0
	v_pk_fma_f32 v[42:43], v[80:81], v[38:39], v[42:43] op_sel_hi:[0,1,1]
	ds_write2_b64 v68, v[30:31], v[42:43] offset1:16
	v_pk_mul_f32 v[30:31], v[14:15], v[38:39] op_sel:[1,1] op_sel_hi:[0,1] neg_lo:[0,1]
	v_pk_fma_f32 v[30:31], v[14:15], v[38:39], v[30:31] op_sel_hi:[1,0,1]
	s_nop 0
	v_pk_mul_f32 v[38:39], v[34:35], v[30:31] op_sel:[1,1] op_sel_hi:[1,0] neg_lo:[1,0]
	s_nop 0
	v_pk_fma_f32 v[34:35], v[34:35], v[30:31], v[38:39] op_sel_hi:[0,1,1]
	v_pk_mul_f32 v[38:39], v[14:15], v[30:31] op_sel:[1,1] op_sel_hi:[0,1] neg_lo:[0,1]
	v_pk_fma_f32 v[30:31], v[14:15], v[30:31], v[38:39] op_sel_hi:[1,0,1]
	s_nop 0
	v_pk_mul_f32 v[38:39], v[54:55], v[30:31] op_sel:[1,1] op_sel_hi:[1,0] neg_lo:[1,0]
	s_nop 0
	v_pk_fma_f32 v[38:39], v[54:55], v[30:31], v[38:39] op_sel_hi:[0,1,1]
	ds_write2_b64 v67, v[34:35], v[38:39] offset0:32 offset1:48
	v_pk_mul_f32 v[34:35], v[14:15], v[30:31] op_sel:[1,1] op_sel_hi:[0,1] neg_lo:[0,1]
	v_pk_fma_f32 v[30:31], v[14:15], v[30:31], v[34:35] op_sel_hi:[1,0,1]
	s_nop 0
	v_pk_mul_f32 v[34:35], v[26:27], v[30:31] op_sel:[1,1] op_sel_hi:[1,0] neg_lo:[1,0]
	s_nop 0
	v_pk_fma_f32 v[26:27], v[26:27], v[30:31], v[34:35] op_sel_hi:[0,1,1]
	v_pk_mul_f32 v[34:35], v[14:15], v[30:31] op_sel:[1,1] op_sel_hi:[0,1] neg_lo:[0,1]
	v_pk_fma_f32 v[30:31], v[14:15], v[30:31], v[34:35] op_sel_hi:[1,0,1]
	s_nop 0
	v_pk_mul_f32 v[34:35], v[48:49], v[30:31] op_sel:[1,1] op_sel_hi:[1,0] neg_lo:[1,0]
	s_nop 0
	v_pk_fma_f32 v[34:35], v[48:49], v[30:31], v[34:35] op_sel_hi:[0,1,1]
	ds_write2_b64 v66, v[26:27], v[34:35] offset0:64 offset1:80
	v_pk_mul_f32 v[26:27], v[14:15], v[30:31] op_sel:[1,1] op_sel_hi:[0,1] neg_lo:[0,1]
	v_pk_fma_f32 v[26:27], v[14:15], v[30:31], v[26:27] op_sel_hi:[1,0,1]
	s_nop 0
	v_pk_mul_f32 v[30:31], v[28:29], v[26:27] op_sel:[1,1] op_sel_hi:[1,0] neg_lo:[1,0]
	s_nop 0
	v_pk_fma_f32 v[28:29], v[28:29], v[26:27], v[30:31] op_sel_hi:[0,1,1]
	v_pk_mul_f32 v[30:31], v[14:15], v[26:27] op_sel:[1,1] op_sel_hi:[0,1] neg_lo:[0,1]
	v_pk_fma_f32 v[26:27], v[14:15], v[26:27], v[30:31] op_sel_hi:[1,0,1]
	s_nop 0
	v_pk_mul_f32 v[30:31], v[52:53], v[26:27] op_sel:[1,1] op_sel_hi:[1,0] neg_lo:[1,0]
	s_nop 0
	v_pk_fma_f32 v[30:31], v[52:53], v[26:27], v[30:31] op_sel_hi:[0,1,1]
	ds_write2_b64 v65, v[28:29], v[30:31] offset0:96 offset1:112
	v_pk_mul_f32 v[28:29], v[14:15], v[26:27] op_sel:[1,1] op_sel_hi:[0,1] neg_lo:[0,1]
	v_pk_fma_f32 v[26:27], v[14:15], v[26:27], v[28:29] op_sel_hi:[1,0,1]
	s_nop 0
	v_pk_mul_f32 v[28:29], v[22:23], v[26:27] op_sel:[1,1] op_sel_hi:[1,0] neg_lo:[1,0]
	s_nop 0
	v_pk_fma_f32 v[22:23], v[22:23], v[26:27], v[28:29] op_sel_hi:[0,1,1]
	v_pk_mul_f32 v[28:29], v[14:15], v[26:27] op_sel:[1,1] op_sel_hi:[0,1] neg_lo:[0,1]
	v_pk_fma_f32 v[26:27], v[14:15], v[26:27], v[28:29] op_sel_hi:[1,0,1]
	s_nop 0
	v_pk_mul_f32 v[28:29], v[40:41], v[26:27] op_sel:[1,1] op_sel_hi:[1,0] neg_lo:[1,0]
	s_nop 0
	v_pk_fma_f32 v[28:29], v[40:41], v[26:27], v[28:29] op_sel_hi:[0,1,1]
	ds_write2_b64 v64, v[22:23], v[28:29] offset0:128 offset1:144
	v_pk_mul_f32 v[22:23], v[14:15], v[26:27] op_sel:[1,1] op_sel_hi:[0,1] neg_lo:[0,1]
	v_pk_fma_f32 v[22:23], v[14:15], v[26:27], v[22:23] op_sel_hi:[1,0,1]
	s_nop 0
	v_pk_mul_f32 v[26:27], v[24:25], v[22:23] op_sel:[1,1] op_sel_hi:[1,0] neg_lo:[1,0]
	s_nop 0
	v_pk_fma_f32 v[24:25], v[24:25], v[22:23], v[26:27] op_sel_hi:[0,1,1]
	v_pk_mul_f32 v[26:27], v[14:15], v[22:23] op_sel:[1,1] op_sel_hi:[0,1] neg_lo:[0,1]
	v_pk_fma_f32 v[22:23], v[14:15], v[22:23], v[26:27] op_sel_hi:[1,0,1]
	s_nop 0
	v_pk_mul_f32 v[26:27], v[44:45], v[22:23] op_sel:[1,1] op_sel_hi:[1,0] neg_lo:[1,0]
	s_nop 0
	v_pk_fma_f32 v[26:27], v[44:45], v[22:23], v[26:27] op_sel_hi:[0,1,1]
	ds_write2_b64 v63, v[24:25], v[26:27] offset0:160 offset1:176
	v_pk_mul_f32 v[24:25], v[14:15], v[22:23] op_sel:[1,1] op_sel_hi:[0,1] neg_lo:[0,1]
	v_pk_fma_f32 v[22:23], v[14:15], v[22:23], v[24:25] op_sel_hi:[1,0,1]
	s_nop 0
	v_pk_mul_f32 v[24:25], v[18:19], v[22:23] op_sel:[1,1] op_sel_hi:[1,0] neg_lo:[1,0]
	s_nop 0
	v_pk_fma_f32 v[18:19], v[18:19], v[22:23], v[24:25] op_sel_hi:[0,1,1]
	v_pk_mul_f32 v[24:25], v[14:15], v[22:23] op_sel:[1,1] op_sel_hi:[0,1] neg_lo:[0,1]
	v_pk_fma_f32 v[22:23], v[14:15], v[22:23], v[24:25] op_sel_hi:[1,0,1]
	s_nop 0
	v_pk_mul_f32 v[24:25], v[32:33], v[22:23] op_sel:[1,1] op_sel_hi:[1,0] neg_lo:[1,0]
	s_nop 0
	v_pk_fma_f32 v[24:25], v[32:33], v[22:23], v[24:25] op_sel_hi:[0,1,1]
	ds_write2_b64 v62, v[18:19], v[24:25] offset0:192 offset1:208
	v_pk_mul_f32 v[18:19], v[14:15], v[22:23] op_sel:[1,1] op_sel_hi:[0,1] neg_lo:[0,1]
	v_pk_fma_f32 v[18:19], v[14:15], v[22:23], v[18:19] op_sel_hi:[1,0,1]
	s_nop 0
	v_pk_mul_f32 v[22:23], v[20:21], v[18:19] op_sel:[1,1] op_sel_hi:[1,0] neg_lo:[1,0]
	s_nop 0
	v_pk_fma_f32 v[20:21], v[20:21], v[18:19], v[22:23] op_sel_hi:[0,1,1]
	v_pk_mul_f32 v[22:23], v[14:15], v[18:19] op_sel:[1,1] op_sel_hi:[0,1] neg_lo:[0,1]
	v_pk_fma_f32 v[14:15], v[14:15], v[18:19], v[22:23] op_sel_hi:[1,0,1]
	s_nop 0
	v_pk_mul_f32 v[18:19], v[36:37], v[14:15] op_sel:[1,1] op_sel_hi:[1,0] neg_lo:[1,0]
	s_nop 0
	v_pk_fma_f32 v[14:15], v[36:37], v[14:15], v[18:19] op_sel_hi:[0,1,1]
	ds_write2_b64 v13, v[20:21], v[14:15] offset0:224 offset1:240
	v_mov_b32_e32 v14, v182
	v_mov_b32_e32 v10, v176
	v_mov_b32_e32 v13, v175
	s_waitcnt lgkmcnt(0)
	s_barrier
	v_mov_b32_e32 v50, v167
	v_xor_b32_e32 v18, 1, v13
	v_lshlrev_b32_e32 v10, 3, v10
	v_lshlrev_b32_e32 v18, 3, v18
	v_add3_u32 v20, 0, v18, v10
	v_xor_b32_e32 v18, 2, v13
	v_lshlrev_b32_e32 v18, 3, v18
	v_xor_b32_e32 v26, 5, v13
	v_add3_u32 v22, 0, v18, v10
	v_xor_b32_e32 v18, 3, v13
	v_lshlrev_b32_e32 v26, 3, v26
	v_lshlrev_b32_e32 v15, 3, v13
	v_lshlrev_b32_e32 v18, 3, v18
	v_add3_u32 v28, 0, v26, v10
	v_xor_b32_e32 v26, 6, v13
	v_add3_u32 v15, 0, v15, v10
	v_add3_u32 v24, 0, v18, v10
	v_lshlrev_b32_e32 v26, 3, v26
	v_xor_b32_e32 v34, 9, v13
	ds_read_b64 v[18:19], v15
	ds_read_b64 v[20:21], v20
	ds_read_b64 v[22:23], v22
	ds_read_b64 v[24:25], v24
	v_xor_b32_e32 v15, 4, v13
	v_add3_u32 v30, 0, v26, v10
	v_xor_b32_e32 v26, 7, v13
	v_lshlrev_b32_e32 v34, 3, v34
	v_lshlrev_b32_e32 v15, 3, v15
	v_lshlrev_b32_e32 v26, 3, v26
	v_add3_u32 v36, 0, v34, v10
	v_xor_b32_e32 v34, 10, v13
	v_add3_u32 v15, 0, v15, v10
	v_add3_u32 v32, 0, v26, v10
	v_lshlrev_b32_e32 v34, 3, v34
	ds_read_b64 v[26:27], v15
	ds_read_b64 v[28:29], v28
	ds_read_b64 v[30:31], v30
	ds_read_b64 v[32:33], v32
	v_xor_b32_e32 v15, 8, v13
	v_add3_u32 v38, 0, v34, v10
	v_xor_b32_e32 v34, 11, v13
	v_lshlrev_b32_e32 v15, 3, v15
	v_lshlrev_b32_e32 v34, 3, v34
	v_xor_b32_e32 v42, 13, v13
	v_add3_u32 v15, 0, v15, v10
	v_add3_u32 v40, 0, v34, v10
	v_lshlrev_b32_e32 v42, 3, v42
	ds_read_b64 v[34:35], v15
	ds_read_b64 v[36:37], v36
	ds_read_b64 v[38:39], v38
	ds_read_b64 v[40:41], v40
	v_xor_b32_e32 v15, 12, v13
	v_add3_u32 v44, 0, v42, v10
	v_xor_b32_e32 v42, 14, v13
	v_xor_b32_e32 v13, 15, v13
	v_lshlrev_b32_e32 v15, 3, v15
	v_lshlrev_b32_e32 v42, 3, v42
	v_lshlrev_b32_e32 v13, 3, v13
	v_add3_u32 v15, 0, v15, v10
	v_add3_u32 v46, 0, v42, v10
	v_add3_u32 v10, 0, v13, v10
	ds_read_b64 v[42:43], v15
	ds_read_b64 v[44:45], v44
	ds_read_b64 v[46:47], v46
	ds_read_b64 v[48:49], v10
	v_mov_b32_e32 v10, v1
	v_mov_b32_e32 v13, v166
	v_mov_b32_e32 v10, v164
	s_waitcnt lgkmcnt(7)
	v_pk_add_f32 v[54:55], v[18:19], v[34:35]
	v_mov_b32_e32 v10, v165
	v_pk_add_f32 v[18:19], v[18:19], v[34:35] neg_lo:[0,1] neg_hi:[0,1]
	s_waitcnt lgkmcnt(6)
	v_pk_add_f32 v[34:35], v[20:21], v[36:37]
	v_pk_add_f32 v[20:21], v[20:21], v[36:37] neg_lo:[0,1] neg_hi:[0,1]
	v_mov_b32_e32 v13, v168
	v_mov_b32_e32 v52, v169
	v_ashrrev_i32_e32 v15, 31, v14
	v_pk_mul_f32 v[36:37], v[20:21], v[52:53] op_sel:[1,0] op_sel_hi:[0,0] neg_lo:[1,1] neg_hi:[0,1]
	v_mov_b32_e32 v13, v170
	v_pk_fma_f32 v[20:21], v[20:21], v[10:11], v[36:37] op_sel_hi:[1,0,1]
	s_waitcnt lgkmcnt(5)
	v_pk_add_f32 v[36:37], v[22:23], v[38:39]
	v_pk_add_f32 v[22:23], v[22:23], v[38:39] neg_lo:[0,1] neg_hi:[0,1]
	s_movk_i32 s0, 0x1000
	v_pk_mul_f32 v[38:39], v[22:23], v[50:51] op_sel:[1,0] op_sel_hi:[0,0] neg_lo:[1,1] neg_hi:[0,1]
	v_mov_b32_e32 v13, v171
	v_pk_fma_f32 v[22:23], v[22:23], v[50:51], v[38:39] op_sel_hi:[1,0,1]
	s_waitcnt lgkmcnt(4)
	v_pk_add_f32 v[38:39], v[24:25], v[40:41]
	v_pk_add_f32 v[24:25], v[24:25], v[40:41] neg_lo:[0,1] neg_hi:[0,1]
	v_mov_b32_e32 v72, v164
	v_pk_mul_f32 v[40:41], v[24:25], v[52:53] op_sel_hi:[1,0]
	s_nop 0
	v_pk_fma_f32 v[24:25], v[24:25], v[10:11], v[40:41] op_sel:[1,0,0] op_sel_hi:[0,0,1] neg_lo:[1,1,0] neg_hi:[0,1,0]
	s_waitcnt lgkmcnt(3)
	v_pk_add_f32 v[40:41], v[26:27], v[42:43]
	v_pk_add_f32 v[26:27], v[26:27], v[42:43] neg_lo:[0,1] neg_hi:[0,1]
	v_mov_b32_e32 v13, v175
	v_xor_b32_e32 v43, 0x80000000, v26
	v_mov_b32_e32 v42, v27
	s_waitcnt lgkmcnt(2)
	v_pk_add_f32 v[26:27], v[28:29], v[44:45]
	v_pk_add_f32 v[28:29], v[28:29], v[44:45] neg_lo:[0,1] neg_hi:[0,1]
	v_mov_b32_e32 v74, v166
	v_pk_mul_f32 v[44:45], v[28:29], v[52:53] op_sel_hi:[1,0] neg_lo:[0,1] neg_hi:[0,1]
	s_nop 0
	v_pk_fma_f32 v[28:29], v[28:29], v[10:11], v[44:45] op_sel:[1,0,0] op_sel_hi:[0,0,1] neg_lo:[1,1,0] neg_hi:[0,1,0]
	s_waitcnt lgkmcnt(1)
	v_pk_add_f32 v[44:45], v[30:31], v[46:47]
	v_pk_add_f32 v[30:31], v[30:31], v[46:47] neg_lo:[0,1] neg_hi:[0,1]
	v_mov_b32_e32 v76, v168
	v_pk_mul_f32 v[46:47], v[30:31], v[50:51] op_sel:[1,0] op_sel_hi:[0,0] neg_lo:[1,1] neg_hi:[0,1]
	v_mov_b32_e32 v78, v170
	v_pk_fma_f32 v[30:31], v[30:31], v[50:51], v[46:47] op_sel_hi:[1,0,1] neg_lo:[0,1,0] neg_hi:[0,1,0]
	s_waitcnt lgkmcnt(0)
	v_pk_add_f32 v[46:47], v[32:33], v[48:49]
	v_pk_add_f32 v[32:33], v[32:33], v[48:49] neg_lo:[0,1] neg_hi:[0,1]
	v_mov_b32_e32 v83, v11
	v_pk_mul_f32 v[48:49], v[32:33], v[52:53] op_sel:[1,0] op_sel_hi:[0,0] neg_lo:[1,1] neg_hi:[0,1]
	v_pk_add_f32 v[52:53], v[34:35], v[26:27]
	v_pk_add_f32 v[26:27], v[34:35], v[26:27] neg_lo:[0,1] neg_hi:[0,1]
	v_pk_fma_f32 v[32:33], v[32:33], v[10:11], v[48:49] op_sel_hi:[1,0,1] neg_lo:[0,1,0] neg_hi:[0,1,0]
	v_pk_mul_f32 v[34:35], v[26:27], v[50:51] op_sel:[1,0] op_sel_hi:[0,0] neg_lo:[1,1] neg_hi:[0,1]
	v_pk_add_f32 v[48:49], v[54:55], v[40:41]
	v_pk_fma_f32 v[26:27], v[26:27], v[50:51], v[34:35] op_sel_hi:[1,0,1]
	v_pk_add_f32 v[34:35], v[36:37], v[44:45]
	v_pk_add_f32 v[36:37], v[36:37], v[44:45] neg_lo:[0,1] neg_hi:[0,1]
	v_pk_add_f32 v[40:41], v[54:55], v[40:41] neg_lo:[0,1] neg_hi:[0,1]
	v_xor_b32_e32 v45, 0x80000000, v36
	v_mov_b32_e32 v44, v37
	v_pk_add_f32 v[36:37], v[38:39], v[46:47]
	v_pk_add_f32 v[38:39], v[38:39], v[46:47] neg_lo:[0,1] neg_hi:[0,1]
	v_mov_b32_e32 v10, v177
	v_pk_mul_f32 v[46:47], v[38:39], v[50:51] op_sel:[1,0] op_sel_hi:[0,0] neg_lo:[1,1] neg_hi:[0,1]
	s_mov_b32 s7, 0xa000
	v_pk_fma_f32 v[38:39], v[38:39], v[50:51], v[46:47] op_sel_hi:[1,0,1] neg_lo:[0,1,0] neg_hi:[0,1,0]
	v_pk_add_f32 v[46:47], v[48:49], v[34:35]
	v_pk_add_f32 v[34:35], v[48:49], v[34:35] neg_lo:[0,1] neg_hi:[0,1]
	v_pk_add_f32 v[48:49], v[52:53], v[36:37]
	v_pk_add_f32 v[36:37], v[52:53], v[36:37] neg_lo:[0,1] neg_hi:[0,1]
	s_mov_b32 s6, 0xc000
	v_xor_b32_e32 v53, 0x80000000, v36
	v_mov_b32_e32 v52, v37
	v_pk_add_f32 v[36:37], v[46:47], v[48:49]
	v_pk_add_f32 v[46:47], v[46:47], v[48:49] neg_lo:[0,1] neg_hi:[0,1]
	v_pk_add_f32 v[48:49], v[34:35], v[52:53]
	v_pk_add_f32 v[34:35], v[34:35], v[52:53] neg_lo:[0,1] neg_hi:[0,1]
	v_pk_add_f32 v[52:53], v[40:41], v[44:45]
	v_pk_add_f32 v[40:41], v[40:41], v[44:45] neg_lo:[0,1] neg_hi:[0,1]
	v_pk_add_f32 v[44:45], v[26:27], v[38:39]
	v_pk_add_f32 v[26:27], v[26:27], v[38:39] neg_lo:[0,1] neg_hi:[0,1]
	s_mov_b32 s1, 0xe000
	v_xor_b32_e32 v39, 0x80000000, v26
	v_mov_b32_e32 v38, v27
	v_pk_add_f32 v[26:27], v[52:53], v[44:45]
	v_pk_add_f32 v[44:45], v[52:53], v[44:45] neg_lo:[0,1] neg_hi:[0,1]
	v_pk_add_f32 v[52:53], v[40:41], v[38:39]
	v_pk_add_f32 v[38:39], v[40:41], v[38:39] neg_lo:[0,1] neg_hi:[0,1]
	v_pk_add_f32 v[40:41], v[18:19], v[42:43]
	v_pk_add_f32 v[18:19], v[18:19], v[42:43] neg_lo:[0,1] neg_hi:[0,1]
	v_pk_add_f32 v[42:43], v[20:21], v[28:29]
	v_pk_add_f32 v[20:21], v[20:21], v[28:29] neg_lo:[0,1] neg_hi:[0,1]
	s_mov_b32 s8, 0x8000
	v_pk_mul_f32 v[28:29], v[50:51], v[20:21] op_sel:[0,1] op_sel_hi:[0,0] neg_lo:[1,1] neg_hi:[1,0]
	v_pk_fma_f32 v[20:21], v[50:51], v[20:21], v[28:29] op_sel_hi:[0,1,1]
	v_pk_add_f32 v[28:29], v[22:23], v[30:31]
	v_pk_add_f32 v[22:23], v[22:23], v[30:31] neg_lo:[0,1] neg_hi:[0,1]
	s_mov_b32 s9, 0x9000
	v_xor_b32_e32 v31, 0x80000000, v22
	v_mov_b32_e32 v30, v23
	v_pk_add_f32 v[22:23], v[24:25], v[32:33]
	v_pk_add_f32 v[24:25], v[24:25], v[32:33] neg_lo:[0,1] neg_hi:[0,1]
	s_mov_b32 s5, 0xb000
	v_pk_mul_f32 v[32:33], v[50:51], v[24:25] op_sel:[0,1] op_sel_hi:[0,0] neg_lo:[1,1] neg_hi:[1,0]
	v_pk_fma_f32 v[24:25], v[50:51], v[24:25], v[32:33] op_sel_hi:[0,1,1] neg_lo:[1,0,0] neg_hi:[1,0,0]
	v_pk_add_f32 v[32:33], v[40:41], v[28:29]
	v_pk_add_f32 v[28:29], v[40:41], v[28:29] neg_lo:[0,1] neg_hi:[0,1]
	v_pk_add_f32 v[40:41], v[42:43], v[22:23]
	v_pk_add_f32 v[22:23], v[42:43], v[22:23] neg_lo:[0,1] neg_hi:[0,1]
	v_mov_b32_e32 v50, v167
	v_xor_b32_e32 v43, 0x80000000, v22
	v_mov_b32_e32 v42, v23
	v_pk_add_f32 v[22:23], v[32:33], v[40:41]
	v_pk_add_f32 v[32:33], v[32:33], v[40:41] neg_lo:[0,1] neg_hi:[0,1]
	v_pk_add_f32 v[40:41], v[28:29], v[42:43]
	v_pk_add_f32 v[28:29], v[28:29], v[42:43] neg_lo:[0,1] neg_hi:[0,1]
	v_pk_add_f32 v[42:43], v[18:19], v[30:31]
	v_pk_add_f32 v[18:19], v[18:19], v[30:31] neg_lo:[0,1] neg_hi:[0,1]
	v_pk_add_f32 v[30:31], v[20:21], v[24:25]
	v_pk_add_f32 v[20:21], v[20:21], v[24:25] neg_lo:[0,1] neg_hi:[0,1]
	s_mov_b32 s4, 0xd000
	v_xor_b32_e32 v25, 0x80000000, v20
	v_mov_b32_e32 v24, v21
	v_pk_add_f32 v[20:21], v[42:43], v[30:31]
	v_pk_add_f32 v[30:31], v[42:43], v[30:31] neg_lo:[0,1] neg_hi:[0,1]
	v_pk_add_f32 v[42:43], v[18:19], v[24:25]
	v_pk_add_f32 v[18:19], v[18:19], v[24:25] neg_lo:[0,1] neg_hi:[0,1]
	v_lshl_add_u64 v[24:25], v[14:15], 3, s[46:47]
	global_store_dwordx2 v[24:25], v[36:37], off
	v_add_u32_e32 v24, 0x200, v14
	v_ashrrev_i32_e32 v25, 31, v24
	v_lshl_add_u64 v[24:25], v[24:25], 3, s[46:47]
	global_store_dwordx2 v[24:25], v[22:23], off
	v_add_u32_e32 v22, 0x400, v14
	v_ashrrev_i32_e32 v23, 31, v22
	v_lshl_add_u64 v[22:23], v[22:23], 3, s[46:47]
	global_store_dwordx2 v[22:23], v[26:27], off
	v_add_u32_e32 v22, 0x600, v14
	v_ashrrev_i32_e32 v23, 31, v22
	v_lshl_add_u64 v[22:23], v[22:23], 3, s[46:47]
	global_store_dwordx2 v[22:23], v[20:21], off
	v_add_u32_e32 v20, 0x800, v14
	v_ashrrev_i32_e32 v21, 31, v20
	v_lshl_add_u64 v[20:21], v[20:21], 3, s[46:47]
	global_store_dwordx2 v[20:21], v[48:49], off
	v_add_u32_e32 v20, 0xa00, v14
	v_ashrrev_i32_e32 v21, 31, v20
	v_lshl_add_u64 v[20:21], v[20:21], 3, s[46:47]
	global_store_dwordx2 v[20:21], v[40:41], off
	v_add_u32_e32 v20, 0xc00, v14
	v_ashrrev_i32_e32 v21, 31, v20
	v_lshl_add_u64 v[20:21], v[20:21], 3, s[46:47]
	global_store_dwordx2 v[20:21], v[52:53], off
	v_add_u32_e32 v20, 0xe00, v14
	v_ashrrev_i32_e32 v21, 31, v20
	v_lshl_add_u64 v[20:21], v[20:21], 3, s[46:47]
	global_store_dwordx2 v[20:21], v[42:43], off
	v_add_u32_e32 v20, 0x1000, v14
	v_ashrrev_i32_e32 v21, 31, v20
	v_lshl_add_u64 v[20:21], v[20:21], 3, s[46:47]
	global_store_dwordx2 v[20:21], v[46:47], off
	v_add_u32_e32 v20, 0x1200, v14
	v_ashrrev_i32_e32 v21, 31, v20
	v_lshl_add_u64 v[20:21], v[20:21], 3, s[46:47]
	global_store_dwordx2 v[20:21], v[32:33], off
	v_add_u32_e32 v20, 0x1400, v14
	v_ashrrev_i32_e32 v21, 31, v20
	v_lshl_add_u64 v[20:21], v[20:21], 3, s[46:47]
	global_store_dwordx2 v[20:21], v[44:45], off
	v_add_u32_e32 v20, 0x1600, v14
	v_ashrrev_i32_e32 v21, 31, v20
	v_lshl_add_u64 v[20:21], v[20:21], 3, s[46:47]
	global_store_dwordx2 v[20:21], v[30:31], off
	v_add_u32_e32 v20, 0x1800, v14
	v_ashrrev_i32_e32 v21, 31, v20
	v_lshl_add_u64 v[20:21], v[20:21], 3, s[46:47]
	global_store_dwordx2 v[20:21], v[34:35], off
	v_add_u32_e32 v20, 0x1a00, v14
	v_ashrrev_i32_e32 v21, 31, v20
	v_lshl_add_u64 v[20:21], v[20:21], 3, s[46:47]
	global_store_dwordx2 v[20:21], v[28:29], off
	v_add_u32_e32 v20, 0x1c00, v14
	v_ashrrev_i32_e32 v21, 31, v20
	v_lshl_add_u64 v[20:21], v[20:21], 3, s[46:47]
	global_store_dwordx2 v[20:21], v[38:39], off
	v_add_u32_e32 v20, 0x1e00, v14
	v_ashrrev_i32_e32 v21, 31, v20
	v_lshl_add_u64 v[20:21], v[20:21], 3, s[46:47]
	global_store_dwordx2 v[20:21], v[18:19], off
	v_mov_b32_e32 v52, v169
	v_xor_b32_e32 v18, 1, v13
	v_lshlrev_b32_e32 v10, 3, v10
	v_lshlrev_b32_e32 v18, 3, v18
	v_add3_u32 v20, 0, v18, v10
	v_xor_b32_e32 v18, 2, v13
	v_lshlrev_b32_e32 v18, 3, v18
	v_xor_b32_e32 v26, 5, v13
	v_add3_u32 v22, 0, v18, v10
	v_xor_b32_e32 v18, 3, v13
	v_lshlrev_b32_e32 v26, 3, v26
	v_lshlrev_b32_e32 v15, 3, v13
	v_lshlrev_b32_e32 v18, 3, v18
	v_add3_u32 v28, 0, v26, v10
	v_xor_b32_e32 v26, 6, v13
	v_add3_u32 v15, 0, v15, v10
	v_add3_u32 v24, 0, v18, v10
	v_lshlrev_b32_e32 v26, 3, v26
	v_xor_b32_e32 v34, 9, v13
	ds_read_b64 v[18:19], v15
	ds_read_b64 v[20:21], v20
	ds_read_b64 v[22:23], v22
	ds_read_b64 v[24:25], v24
	v_xor_b32_e32 v15, 4, v13
	v_add3_u32 v30, 0, v26, v10
	v_xor_b32_e32 v26, 7, v13
	v_lshlrev_b32_e32 v34, 3, v34
	v_lshlrev_b32_e32 v15, 3, v15
	v_lshlrev_b32_e32 v26, 3, v26
	v_add3_u32 v36, 0, v34, v10
	v_xor_b32_e32 v34, 10, v13
	v_add3_u32 v15, 0, v15, v10
	v_add3_u32 v32, 0, v26, v10
	v_lshlrev_b32_e32 v34, 3, v34
	ds_read_b64 v[26:27], v15
	ds_read_b64 v[28:29], v28
	ds_read_b64 v[30:31], v30
	ds_read_b64 v[32:33], v32
	v_xor_b32_e32 v15, 8, v13
	v_add3_u32 v38, 0, v34, v10
	v_xor_b32_e32 v34, 11, v13
	v_lshlrev_b32_e32 v15, 3, v15
	v_lshlrev_b32_e32 v34, 3, v34
	v_xor_b32_e32 v42, 13, v13
	v_add3_u32 v15, 0, v15, v10
	v_add3_u32 v40, 0, v34, v10
	v_lshlrev_b32_e32 v42, 3, v42
	ds_read_b64 v[34:35], v15
	ds_read_b64 v[36:37], v36
	ds_read_b64 v[38:39], v38
	ds_read_b64 v[40:41], v40
	v_xor_b32_e32 v15, 12, v13
	v_add3_u32 v44, 0, v42, v10
	v_xor_b32_e32 v42, 14, v13
	v_xor_b32_e32 v13, 15, v13
	v_lshlrev_b32_e32 v15, 3, v15
	v_lshlrev_b32_e32 v42, 3, v42
	v_lshlrev_b32_e32 v13, 3, v13
	v_add3_u32 v15, 0, v15, v10
	v_add3_u32 v46, 0, v42, v10
	v_add3_u32 v10, 0, v13, v10
	ds_read_b64 v[42:43], v15
	ds_read_b64 v[44:45], v44
	ds_read_b64 v[46:47], v46
	ds_read_b64 v[48:49], v10
	v_mov_b32_e32 v10, v1
	v_mov_b32_e32 v13, v166
	v_mov_b32_e32 v10, v164
	s_waitcnt lgkmcnt(7)
	v_pk_add_f32 v[54:55], v[18:19], v[34:35]
	v_mov_b32_e32 v10, v165
	v_pk_add_f32 v[18:19], v[18:19], v[34:35] neg_lo:[0,1] neg_hi:[0,1]
	s_waitcnt lgkmcnt(6)
	v_pk_add_f32 v[34:35], v[20:21], v[36:37]
	v_pk_add_f32 v[20:21], v[20:21], v[36:37] neg_lo:[0,1] neg_hi:[0,1]
	v_mov_b32_e32 v13, v168
	s_nop 0
	v_pk_mul_f32 v[36:37], v[20:21], v[52:53] op_sel:[1,0] op_sel_hi:[0,0] neg_lo:[1,1] neg_hi:[0,1]
	v_mov_b32_e32 v13, v170
	v_pk_fma_f32 v[20:21], v[20:21], v[10:11], v[36:37] op_sel_hi:[1,0,1]
	s_waitcnt lgkmcnt(5)
	v_pk_add_f32 v[36:37], v[22:23], v[38:39]
	v_pk_add_f32 v[22:23], v[22:23], v[38:39] neg_lo:[0,1] neg_hi:[0,1]
	s_nop 0
	v_pk_mul_f32 v[38:39], v[22:23], v[50:51] op_sel:[1,0] op_sel_hi:[0,0] neg_lo:[1,1] neg_hi:[0,1]
	v_mov_b32_e32 v13, v171
	v_pk_fma_f32 v[22:23], v[22:23], v[50:51], v[38:39] op_sel_hi:[1,0,1]
	s_waitcnt lgkmcnt(4)
	v_pk_add_f32 v[38:39], v[24:25], v[40:41]
	v_pk_add_f32 v[24:25], v[24:25], v[40:41] neg_lo:[0,1] neg_hi:[0,1]
	s_nop 0
	v_pk_mul_f32 v[40:41], v[24:25], v[52:53] op_sel_hi:[1,0]
	s_nop 0
	v_pk_fma_f32 v[24:25], v[24:25], v[10:11], v[40:41] op_sel:[1,0,0] op_sel_hi:[0,0,1] neg_lo:[1,1,0] neg_hi:[0,1,0]
	s_waitcnt lgkmcnt(3)
	v_pk_add_f32 v[40:41], v[26:27], v[42:43]
	v_pk_add_f32 v[26:27], v[26:27], v[42:43] neg_lo:[0,1] neg_hi:[0,1]
	s_nop 0
	v_xor_b32_e32 v43, 0x80000000, v26
	v_mov_b32_e32 v42, v27
	s_waitcnt lgkmcnt(2)
	v_pk_add_f32 v[26:27], v[28:29], v[44:45]
	v_pk_add_f32 v[28:29], v[28:29], v[44:45] neg_lo:[0,1] neg_hi:[0,1]
	s_nop 0
	v_pk_mul_f32 v[44:45], v[28:29], v[52:53] op_sel_hi:[1,0] neg_lo:[0,1] neg_hi:[0,1]
	s_nop 0
	v_pk_fma_f32 v[28:29], v[28:29], v[10:11], v[44:45] op_sel:[1,0,0] op_sel_hi:[0,0,1] neg_lo:[1,1,0] neg_hi:[0,1,0]
	s_waitcnt lgkmcnt(1)
	v_pk_add_f32 v[44:45], v[30:31], v[46:47]
	v_pk_add_f32 v[30:31], v[30:31], v[46:47] neg_lo:[0,1] neg_hi:[0,1]
	s_nop 0
	v_pk_mul_f32 v[46:47], v[30:31], v[50:51] op_sel:[1,0] op_sel_hi:[0,0] neg_lo:[1,1] neg_hi:[0,1]
	s_nop 0
	v_pk_fma_f32 v[30:31], v[30:31], v[50:51], v[46:47] op_sel_hi:[1,0,1] neg_lo:[0,1,0] neg_hi:[0,1,0]
	s_waitcnt lgkmcnt(0)
	v_pk_add_f32 v[46:47], v[32:33], v[48:49]
	v_pk_add_f32 v[32:33], v[32:33], v[48:49] neg_lo:[0,1] neg_hi:[0,1]
	s_nop 0
	v_pk_mul_f32 v[48:49], v[32:33], v[52:53] op_sel:[1,0] op_sel_hi:[0,0] neg_lo:[1,1] neg_hi:[0,1]
	v_pk_add_f32 v[52:53], v[34:35], v[26:27]
	v_pk_add_f32 v[26:27], v[34:35], v[26:27] neg_lo:[0,1] neg_hi:[0,1]
	v_pk_fma_f32 v[32:33], v[32:33], v[10:11], v[48:49] op_sel_hi:[1,0,1] neg_lo:[0,1,0] neg_hi:[0,1,0]
	v_pk_mul_f32 v[34:35], v[26:27], v[50:51] op_sel:[1,0] op_sel_hi:[0,0] neg_lo:[1,1] neg_hi:[0,1]
	v_pk_add_f32 v[48:49], v[54:55], v[40:41]
	v_pk_fma_f32 v[26:27], v[26:27], v[50:51], v[34:35] op_sel_hi:[1,0,1]
	v_pk_add_f32 v[34:35], v[36:37], v[44:45]
	v_pk_add_f32 v[36:37], v[36:37], v[44:45] neg_lo:[0,1] neg_hi:[0,1]
	v_pk_add_f32 v[40:41], v[54:55], v[40:41] neg_lo:[0,1] neg_hi:[0,1]
	v_xor_b32_e32 v45, 0x80000000, v36
	v_mov_b32_e32 v44, v37
	v_pk_add_f32 v[36:37], v[38:39], v[46:47]
	v_pk_add_f32 v[38:39], v[38:39], v[46:47] neg_lo:[0,1] neg_hi:[0,1]
	v_mov_b32_e32 v10, v1
	v_pk_mul_f32 v[46:47], v[38:39], v[50:51] op_sel:[1,0] op_sel_hi:[0,0] neg_lo:[1,1] neg_hi:[0,1]
	s_nop 0
	v_pk_fma_f32 v[38:39], v[38:39], v[50:51], v[46:47] op_sel_hi:[1,0,1] neg_lo:[0,1,0] neg_hi:[0,1,0]
	v_pk_add_f32 v[46:47], v[48:49], v[34:35]
	v_pk_add_f32 v[34:35], v[48:49], v[34:35] neg_lo:[0,1] neg_hi:[0,1]
	v_pk_add_f32 v[48:49], v[52:53], v[36:37]
	v_pk_add_f32 v[36:37], v[52:53], v[36:37] neg_lo:[0,1] neg_hi:[0,1]
	s_nop 0
	v_xor_b32_e32 v53, 0x80000000, v36
	v_mov_b32_e32 v52, v37
	v_pk_add_f32 v[36:37], v[46:47], v[48:49]
	v_pk_add_f32 v[46:47], v[46:47], v[48:49] neg_lo:[0,1] neg_hi:[0,1]
	v_pk_add_f32 v[48:49], v[34:35], v[52:53]
	v_pk_add_f32 v[34:35], v[34:35], v[52:53] neg_lo:[0,1] neg_hi:[0,1]
	v_pk_add_f32 v[52:53], v[40:41], v[44:45]
	v_pk_add_f32 v[40:41], v[40:41], v[44:45] neg_lo:[0,1] neg_hi:[0,1]
	v_pk_add_f32 v[44:45], v[26:27], v[38:39]
	v_pk_add_f32 v[26:27], v[26:27], v[38:39] neg_lo:[0,1] neg_hi:[0,1]
	s_nop 0
	v_xor_b32_e32 v39, 0x80000000, v26
	v_mov_b32_e32 v38, v27
	v_pk_add_f32 v[26:27], v[52:53], v[44:45]
	v_pk_add_f32 v[44:45], v[52:53], v[44:45] neg_lo:[0,1] neg_hi:[0,1]
	v_pk_add_f32 v[52:53], v[40:41], v[38:39]
	v_pk_add_f32 v[38:39], v[40:41], v[38:39] neg_lo:[0,1] neg_hi:[0,1]
	v_pk_add_f32 v[40:41], v[18:19], v[42:43]
	v_pk_add_f32 v[18:19], v[18:19], v[42:43] neg_lo:[0,1] neg_hi:[0,1]
	v_pk_add_f32 v[42:43], v[20:21], v[28:29]
	v_pk_add_f32 v[20:21], v[20:21], v[28:29] neg_lo:[0,1] neg_hi:[0,1]
	s_nop 0
	v_pk_mul_f32 v[28:29], v[50:51], v[20:21] op_sel:[0,1] op_sel_hi:[0,0] neg_lo:[1,1] neg_hi:[1,0]
	v_pk_fma_f32 v[20:21], v[50:51], v[20:21], v[28:29] op_sel_hi:[0,1,1]
	v_pk_add_f32 v[28:29], v[22:23], v[30:31]
	v_pk_add_f32 v[22:23], v[22:23], v[30:31] neg_lo:[0,1] neg_hi:[0,1]
	s_nop 0
	v_xor_b32_e32 v31, 0x80000000, v22
	v_mov_b32_e32 v30, v23
	v_pk_add_f32 v[22:23], v[24:25], v[32:33]
	v_pk_add_f32 v[24:25], v[24:25], v[32:33] neg_lo:[0,1] neg_hi:[0,1]
	s_nop 0
	v_pk_mul_f32 v[32:33], v[50:51], v[24:25] op_sel:[0,1] op_sel_hi:[0,0] neg_lo:[1,1] neg_hi:[1,0]
	v_pk_fma_f32 v[24:25], v[50:51], v[24:25], v[32:33] op_sel_hi:[0,1,1] neg_lo:[1,0,0] neg_hi:[1,0,0]
	v_pk_add_f32 v[32:33], v[40:41], v[28:29]
	v_pk_add_f32 v[28:29], v[40:41], v[28:29] neg_lo:[0,1] neg_hi:[0,1]
	v_pk_add_f32 v[40:41], v[42:43], v[22:23]
	v_pk_add_f32 v[22:23], v[42:43], v[22:23] neg_lo:[0,1] neg_hi:[0,1]
	s_nop 0
	v_xor_b32_e32 v43, 0x80000000, v22
	v_mov_b32_e32 v42, v23
	v_pk_add_f32 v[22:23], v[32:33], v[40:41]
	v_pk_add_f32 v[32:33], v[32:33], v[40:41] neg_lo:[0,1] neg_hi:[0,1]
	v_pk_add_f32 v[40:41], v[28:29], v[42:43]
	v_pk_add_f32 v[28:29], v[28:29], v[42:43] neg_lo:[0,1] neg_hi:[0,1]
	v_pk_add_f32 v[42:43], v[18:19], v[30:31]
	v_pk_add_f32 v[18:19], v[18:19], v[30:31] neg_lo:[0,1] neg_hi:[0,1]
	v_pk_add_f32 v[30:31], v[20:21], v[24:25]
	v_pk_add_f32 v[20:21], v[20:21], v[24:25] neg_lo:[0,1] neg_hi:[0,1]
	s_nop 0
	v_xor_b32_e32 v25, 0x80000000, v20
	v_mov_b32_e32 v24, v21
	v_pk_add_f32 v[20:21], v[42:43], v[30:31]
	v_pk_add_f32 v[30:31], v[42:43], v[30:31] neg_lo:[0,1] neg_hi:[0,1]
	v_pk_add_f32 v[42:43], v[18:19], v[24:25]
	v_pk_add_f32 v[18:19], v[18:19], v[24:25] neg_lo:[0,1] neg_hi:[0,1]
	v_add_u32_e32 v24, 0x2000, v14
	v_ashrrev_i32_e32 v25, 31, v24
	v_lshl_add_u64 v[24:25], v[24:25], 3, s[46:47]
	global_store_dwordx2 v[24:25], v[36:37], off
	v_add_u32_e32 v24, 0x2200, v14
	v_ashrrev_i32_e32 v25, 31, v24
	v_lshl_add_u64 v[24:25], v[24:25], 3, s[46:47]
	global_store_dwordx2 v[24:25], v[22:23], off
	v_add_u32_e32 v22, 0x2400, v14
	v_ashrrev_i32_e32 v23, 31, v22
	v_lshl_add_u64 v[22:23], v[22:23], 3, s[46:47]
	global_store_dwordx2 v[22:23], v[26:27], off
	v_add_u32_e32 v22, 0x2600, v14
	v_ashrrev_i32_e32 v23, 31, v22
	v_lshl_add_u64 v[22:23], v[22:23], 3, s[46:47]
	global_store_dwordx2 v[22:23], v[20:21], off
	v_add_u32_e32 v20, 0x2800, v14
	v_ashrrev_i32_e32 v21, 31, v20
	v_lshl_add_u64 v[20:21], v[20:21], 3, s[46:47]
	global_store_dwordx2 v[20:21], v[48:49], off
	v_add_u32_e32 v20, 0x2a00, v14
	v_ashrrev_i32_e32 v21, 31, v20
	v_lshl_add_u64 v[20:21], v[20:21], 3, s[46:47]
	global_store_dwordx2 v[20:21], v[40:41], off
	v_add_u32_e32 v20, 0x2c00, v14
	v_ashrrev_i32_e32 v21, 31, v20
	v_lshl_add_u64 v[20:21], v[20:21], 3, s[46:47]
	global_store_dwordx2 v[20:21], v[52:53], off
	v_add_u32_e32 v20, 0x2e00, v14
	v_ashrrev_i32_e32 v21, 31, v20
	v_lshl_add_u64 v[20:21], v[20:21], 3, s[46:47]
	global_store_dwordx2 v[20:21], v[42:43], off
	v_add_u32_e32 v20, 0x3000, v14
	v_ashrrev_i32_e32 v21, 31, v20
	v_lshl_add_u64 v[20:21], v[20:21], 3, s[46:47]
	global_store_dwordx2 v[20:21], v[46:47], off
	v_add_u32_e32 v20, 0x3200, v14
	v_ashrrev_i32_e32 v21, 31, v20
	v_lshl_add_u64 v[20:21], v[20:21], 3, s[46:47]
	global_store_dwordx2 v[20:21], v[32:33], off
	v_add_u32_e32 v20, 0x3400, v14
	v_ashrrev_i32_e32 v21, 31, v20
	v_lshl_add_u64 v[20:21], v[20:21], 3, s[46:47]
	global_store_dwordx2 v[20:21], v[44:45], off
	v_add_u32_e32 v20, 0x3600, v14
	v_ashrrev_i32_e32 v21, 31, v20
	v_lshl_add_u64 v[20:21], v[20:21], 3, s[46:47]
	global_store_dwordx2 v[20:21], v[30:31], off
	v_add_u32_e32 v20, 0x3800, v14
	v_ashrrev_i32_e32 v21, 31, v20
	v_lshl_add_u64 v[20:21], v[20:21], 3, s[46:47]
	global_store_dwordx2 v[20:21], v[34:35], off
	v_add_u32_e32 v20, 0x3a00, v14
	v_ashrrev_i32_e32 v21, 31, v20
	v_lshl_add_u64 v[20:21], v[20:21], 3, s[46:47]
	global_store_dwordx2 v[20:21], v[28:29], off
	v_add_u32_e32 v20, 0x3c00, v14
	v_add_u32_e32 v14, 0x3e00, v14
	v_ashrrev_i32_e32 v15, 31, v14
	v_ashrrev_i32_e32 v21, 31, v20
	v_lshl_add_u64 v[14:15], v[14:15], 3, s[46:47]
	v_lshl_add_u64 v[20:21], v[20:21], 3, s[46:47]
	global_store_dwordx2 v[14:15], v[18:19], off
	v_mov_b32_e32 v14, v182
	global_store_dwordx2 v[20:21], v[38:39], off
	s_barrier
	v_mov_b32_e32 v40, v169
	v_ashrrev_i32_e32 v15, 31, v14
	v_lshl_add_u64 v[18:19], v[14:15], 2, s[64:65]
	v_add_co_u32_e32 v28, vcc, s0, v18
	s_movk_i32 s0, 0x2000
	s_nop 0
	v_addc_co_u32_e32 v29, vcc, 0, v19, vcc
	v_add_co_u32_e32 v22, vcc, s0, v18
	s_movk_i32 s0, 0x6000
	s_nop 0
	v_addc_co_u32_e32 v23, vcc, 0, v19, vcc
	v_add_co_u32_e32 v30, vcc, s78, v18
	global_load_dword v20, v[18:19], off
	global_load_dword v21, v[18:19], off offset:2048
	v_addc_co_u32_e32 v31, vcc, 0, v19, vcc
	v_add_co_u32_e32 v32, vcc, s43, v18
	v_mov_b32_e32 v15, v173
	s_nop 0
	v_addc_co_u32_e32 v33, vcc, 0, v19, vcc
	v_add_co_u32_e32 v34, vcc, s0, v18
	s_mov_b32 s0, 0x8000
	s_nop 0
	v_addc_co_u32_e32 v35, vcc, 0, v19, vcc
	v_add_co_u32_e32 v36, vcc, s0, v18
	s_mov_b32 s0, 0xa000
	s_nop 0
	v_addc_co_u32_e32 v37, vcc, 0, v19, vcc
	v_add_co_u32_e32 v38, vcc, s0, v18
	global_load_dword v26, v[22:23], off offset:-4096
	global_load_dword v24, v[22:23], off
	global_load_dword v25, v[22:23], off offset:2048
	s_nop 0
	global_load_dword v22, v[32:33], off offset:-4096
	v_addc_co_u32_e32 v39, vcc, 0, v19, vcc
	global_load_dword v43, v[32:33], off offset:2048
	global_load_dword v46, v[34:35], off offset:-4096
	global_load_dword v48, v[36:37], off
	global_load_dword v49, v[36:37], off offset:2048
	global_load_dword v62, v[34:35], off
	global_load_dword v63, v[34:35], off offset:2048
	s_nop 0
	global_load_dword v34, v[38:39], off offset:-4096
	global_load_dword v64, v[36:37], off offset:-4096
	s_mov_b32 s0, 0x9000
	v_add_co_u32_e32 v36, vcc, s0, v18
	s_movk_i32 s0, 0x5000
	s_nop 0
	v_addc_co_u32_e32 v37, vcc, 0, v19, vcc
	global_load_dword v27, v[28:29], off offset:2048
	global_load_dword v35, v[36:37], off offset:2048
	v_add_co_u32_e32 v28, vcc, s0, v18
	s_mov_b32 s0, 0xb000
	s_nop 0
	v_addc_co_u32_e32 v29, vcc, 0, v19, vcc
	global_load_dword v66, v[38:39], off
	global_load_dword v67, v[38:39], off offset:2048
	v_add_co_u32_e32 v36, vcc, s0, v18
	s_mov_b32 s0, 0xc000
	s_nop 0
	v_addc_co_u32_e32 v37, vcc, 0, v19, vcc
	v_add_co_u32_e32 v38, vcc, s0, v18
	s_movk_i32 s0, 0x7000
	s_nop 0
	v_addc_co_u32_e32 v39, vcc, 0, v19, vcc
	global_load_dword v68, v[38:39], off offset:-4096
	global_load_dword v23, v[30:31], off offset:2048
	global_load_dword v69, v[36:37], off offset:2048
	v_add_co_u32_e32 v30, vcc, s0, v18
	s_mov_b32 s0, 0xe000
	s_nop 0
	v_addc_co_u32_e32 v31, vcc, 0, v19, vcc
	global_load_dword v47, v[28:29], off offset:2048
	global_load_dword v65, v[30:31], off offset:2048
	global_load_dword v42, v[32:33], off
	s_nop 0
	global_load_dword v30, v[38:39], off
	global_load_dword v31, v[38:39], off offset:2048
	v_add_co_u32_e32 v28, vcc, s0, v18
	s_mov_b32 s0, 0xd000
	s_nop 0
	v_addc_co_u32_e32 v29, vcc, 0, v19, vcc
	global_load_dword v32, v[28:29], off offset:-4096
	v_add_co_u32_e32 v36, vcc, s0, v18
	s_mov_b32 s0, 0xf000
	s_nop 0
	v_addc_co_u32_e32 v37, vcc, 0, v19, vcc
	global_load_dword v33, v[36:37], off offset:2048
	global_load_dword v38, v[28:29], off
	global_load_dword v39, v[28:29], off offset:2048
	v_add_co_u32_e32 v18, vcc, s0, v18
	v_mov_b32_e32 v36, v165
	s_nop 0
	v_addc_co_u32_e32 v19, vcc, 0, v19, vcc
	global_load_dword v70, v[18:19], off
	global_load_dword v71, v[18:19], off offset:2048
	v_mov_b32_e32 v28, v167
	v_mov_b32_e32 v45, v11
	v_mov_b32_e32 v10, v171
	s_waitcnt vmcnt(22)
	v_sub_f32_e32 v44, v21, v49
	v_mov_b32_e32 v13, v44
	v_pk_mul_f32 v[50:51], v[12:13], v[78:79] op_sel_hi:[1,0] neg_lo:[0,1] neg_hi:[0,1]
	v_sub_f32_e32 v10, v20, v48
	v_pk_fma_f32 v[44:45], v[44:45], v[72:73], v[50:51] op_sel_hi:[1,0,1]
	s_waitcnt vmcnt(19)
	v_sub_f32_e32 v50, v26, v34
	v_mov_b32_e32 v13, v50
	v_mov_b32_e32 v51, v11
	v_pk_mul_f32 v[52:53], v[12:13], v[40:41] op_sel_hi:[1,0] neg_lo:[0,1] neg_hi:[0,1]
	v_pk_add_f32 v[20:21], v[20:21], v[48:49]
	v_pk_fma_f32 v[50:51], v[50:51], v[36:37], v[52:53] op_sel_hi:[1,0,1]
	s_waitcnt vmcnt(16)
	v_sub_f32_e32 v52, v27, v35
	v_mov_b32_e32 v13, v52
	v_mov_b32_e32 v53, v11
	v_pk_mul_f32 v[54:55], v[12:13], v[76:77] op_sel_hi:[1,0] neg_lo:[0,1] neg_hi:[0,1]
	v_pk_add_f32 v[26:27], v[26:27], v[34:35]
	v_pk_fma_f32 v[54:55], v[52:53], v[74:75], v[54:55] op_sel_hi:[1,0,1]
	s_waitcnt vmcnt(15)
	v_sub_f32_e32 v52, v24, v66
	v_mov_b32_e32 v13, v52
	v_pk_mul_f32 v[56:57], v[12:13], v[28:29] op_sel_hi:[1,0] neg_lo:[0,1] neg_hi:[0,1]
	s_waitcnt vmcnt(6)
	v_sub_f32_e32 v82, v43, v31
	v_pk_fma_f32 v[56:57], v[52:53], v[28:29], v[56:57] op_sel_hi:[1,0,1]
	v_sub_f32_e32 v52, v25, v67
	v_pk_mul_f32 v[58:59], v[52:53], v[76:77] op_sel_hi:[1,0]
	v_mov_b32_e32 v13, v52
	v_sub_f32_e32 v52, v22, v68
	v_pk_fma_f32 v[60:61], v[12:13], v[74:75], v[58:59] op_sel_hi:[1,0,1] neg_lo:[0,1,0] neg_hi:[0,1,0]
	v_pk_mul_f32 v[58:59], v[52:53], v[40:41] op_sel_hi:[1,0]
	v_mov_b32_e32 v13, v52
	v_sub_f32_e32 v52, v23, v69
	v_pk_fma_f32 v[58:59], v[12:13], v[36:37], v[58:59] op_sel_hi:[1,0,1] neg_lo:[0,1,0] neg_hi:[0,1,0]
	v_pk_mul_f32 v[80:81], v[52:53], v[78:79] op_sel_hi:[1,0]
	v_mov_b32_e32 v13, v52
	v_pk_fma_f32 v[52:53], v[12:13], v[72:73], v[80:81] op_sel_hi:[1,0,1] neg_lo:[0,1,0] neg_hi:[0,1,0]
	v_sub_f32_e32 v13, v42, v30
	v_xor_b32_e32 v81, 0x80000000, v13
	v_pk_mul_f32 v[84:85], v[82:83], v[78:79] op_sel_hi:[1,0] neg_lo:[0,1] neg_hi:[0,1]
	v_mov_b32_e32 v13, v82
	v_pk_fma_f32 v[82:83], v[12:13], v[72:73], v[84:85] op_sel_hi:[1,0,1] neg_lo:[0,1,0] neg_hi:[0,1,0]
	s_waitcnt vmcnt(5)
	v_sub_f32_e32 v84, v46, v32
	v_mov_b32_e32 v85, v11
	v_pk_mul_f32 v[86:87], v[84:85], v[40:41] op_sel_hi:[1,0] neg_lo:[0,1] neg_hi:[0,1]
	v_mov_b32_e32 v13, v84
	v_pk_fma_f32 v[84:85], v[12:13], v[36:37], v[86:87] op_sel_hi:[1,0,1] neg_lo:[0,1,0] neg_hi:[0,1,0]
	s_waitcnt vmcnt(4)
	v_sub_f32_e32 v86, v47, v33
	v_mov_b32_e32 v87, v11
	v_pk_mul_f32 v[88:89], v[86:87], v[76:77] op_sel_hi:[1,0] neg_lo:[0,1] neg_hi:[0,1]
	v_mov_b32_e32 v13, v86
	v_pk_fma_f32 v[86:87], v[12:13], v[74:75], v[88:89] op_sel_hi:[1,0,1] neg_lo:[0,1,0] neg_hi:[0,1,0]
	s_waitcnt vmcnt(3)
	v_sub_f32_e32 v88, v62, v38
	v_mov_b32_e32 v13, v88
	v_mov_b32_e32 v89, v11
	v_pk_mul_f32 v[90:91], v[12:13], v[28:29] op_sel_hi:[1,0] neg_lo:[0,1] neg_hi:[0,1]
	v_pk_add_f32 v[30:31], v[42:43], v[30:31]
	v_pk_fma_f32 v[88:89], v[88:89], v[28:29], v[90:91] op_sel_hi:[1,0,1] neg_lo:[0,1,0] neg_hi:[0,1,0]
	s_waitcnt vmcnt(2)
	v_sub_f32_e32 v90, v63, v39
	v_mov_b32_e32 v13, v90
	v_mov_b32_e32 v91, v11
	v_pk_mul_f32 v[76:77], v[12:13], v[76:77] op_sel_hi:[1,0] neg_lo:[0,1] neg_hi:[0,1]
	v_pk_add_f32 v[42:43], v[20:21], v[30:31] neg_lo:[0,1] neg_hi:[0,1]
	v_pk_fma_f32 v[74:75], v[90:91], v[74:75], v[76:77] op_sel_hi:[1,0,1] neg_lo:[0,1,0] neg_hi:[0,1,0]
	s_waitcnt vmcnt(1)
	v_sub_f32_e32 v76, v64, v70
	v_mov_b32_e32 v13, v76
	v_mov_b32_e32 v77, v11
	v_pk_mul_f32 v[90:91], v[12:13], v[40:41] op_sel_hi:[1,0] neg_lo:[0,1] neg_hi:[0,1]
	v_pk_add_f32 v[32:33], v[46:47], v[32:33]
	v_pk_fma_f32 v[76:77], v[76:77], v[36:37], v[90:91] op_sel_hi:[1,0,1] neg_lo:[0,1,0] neg_hi:[0,1,0]
	s_waitcnt vmcnt(0)
	v_sub_f32_e32 v90, v65, v71
	v_mov_b32_e32 v13, v90
	v_pk_mul_f32 v[78:79], v[12:13], v[78:79] op_sel_hi:[1,0] neg_lo:[0,1] neg_hi:[0,1]
	v_mov_b32_e32 v13, v43
	v_mov_b32_e32 v46, v42
	v_pk_add_f32 v[20:21], v[20:21], v[30:31]
	v_mov_b32_e32 v30, v43
	v_mov_b32_e32 v31, v11
	v_pk_mul_f32 v[42:43], v[12:13], v[40:41] op_sel_hi:[1,0] neg_lo:[0,1] neg_hi:[0,1]
	v_pk_add_f32 v[34:35], v[62:63], v[38:39]
	v_pk_fma_f32 v[62:63], v[30:31], v[36:37], v[42:43] op_sel_hi:[1,0,1]
	v_pk_add_f32 v[30:31], v[26:27], v[32:33] neg_lo:[0,1] neg_hi:[0,1]
	v_pk_add_f32 v[24:25], v[24:25], v[66:67]
	v_mov_b32_e32 v13, v30
	v_mov_b32_e32 v42, v30
	v_pk_mul_f32 v[48:49], v[12:13], v[28:29] op_sel_hi:[1,0] neg_lo:[0,1] neg_hi:[0,1]
	v_pk_add_f32 v[26:27], v[26:27], v[32:33]
	v_mov_b32_e32 v32, v31
	v_mov_b32_e32 v33, v11
	v_mov_b32_e32 v13, v31
	v_pk_add_f32 v[30:31], v[24:25], v[34:35] neg_lo:[0,1] neg_hi:[0,1]
	v_pk_add_f32 v[22:23], v[22:23], v[68:69]
	v_pk_add_f32 v[38:39], v[64:65], v[70:71]
	v_pk_mul_f32 v[32:33], v[32:33], v[40:41] op_sel_hi:[1,0]
	v_pk_add_f32 v[24:25], v[24:25], v[34:35]
	v_mov_b32_e32 v34, v31
	v_mov_b32_e32 v35, v11
	v_pk_fma_f32 v[32:33], v[12:13], v[36:37], v[32:33] op_sel_hi:[1,0,1] neg_lo:[0,1,0] neg_hi:[0,1,0]
	v_xor_b32_e32 v67, 0x80000000, v30
	v_pk_mul_f32 v[34:35], v[34:35], v[40:41] op_sel_hi:[1,0] neg_lo:[0,1] neg_hi:[0,1]
	v_mov_b32_e32 v13, v31
	v_pk_add_f32 v[30:31], v[22:23], v[38:39] neg_lo:[0,1] neg_hi:[0,1]
	v_mov_b32_e32 v43, v11
	v_pk_fma_f32 v[68:69], v[12:13], v[36:37], v[34:35] op_sel_hi:[1,0,1] neg_lo:[0,1,0] neg_hi:[0,1,0]
	v_mov_b32_e32 v13, v30
	v_pk_fma_f32 v[64:65], v[42:43], v[28:29], v[48:49] op_sel_hi:[1,0,1]
	v_mov_b32_e32 v34, v30
	v_mov_b32_e32 v35, v11
	v_pk_mul_f32 v[42:43], v[12:13], v[28:29] op_sel_hi:[1,0] neg_lo:[0,1] neg_hi:[0,1]
	v_mov_b32_e32 v13, v31
	v_pk_fma_f32 v[70:71], v[34:35], v[28:29], v[42:43] op_sel_hi:[1,0,1] neg_lo:[0,1,0] neg_hi:[0,1,0]
	v_mov_b32_e32 v34, v31
	v_pk_mul_f32 v[30:31], v[12:13], v[40:41] op_sel_hi:[1,0] neg_lo:[0,1] neg_hi:[0,1]
	v_pk_add_f32 v[22:23], v[22:23], v[38:39]
	v_pk_fma_f32 v[38:39], v[34:35], v[36:37], v[30:31] op_sel_hi:[1,0,1] neg_lo:[0,1,0] neg_hi:[0,1,0]
	v_pk_add_f32 v[30:31], v[20:21], v[24:25] neg_lo:[0,1] neg_hi:[0,1]
	v_pk_add_f32 v[20:21], v[20:21], v[24:25]
	v_mov_b32_e32 v13, v31
	v_mov_b32_e32 v42, v30
	v_mov_b32_e32 v24, v31
	v_mov_b32_e32 v25, v11
	v_pk_mul_f32 v[30:31], v[12:13], v[28:29] op_sel_hi:[1,0] neg_lo:[0,1] neg_hi:[0,1]
	v_mov_b32_e32 v91, v11
	v_pk_fma_f32 v[30:31], v[24:25], v[28:29], v[30:31] op_sel_hi:[1,0,1]
	v_pk_add_f32 v[24:25], v[26:27], v[22:23] neg_lo:[0,1] neg_hi:[0,1]
	v_pk_fma_f32 v[72:73], v[90:91], v[72:73], v[78:79] op_sel_hi:[1,0,1] neg_lo:[0,1,0] neg_hi:[0,1,0]
	v_mov_b32_e32 v13, v25
	v_xor_b32_e32 v79, 0x80000000, v24
	v_pk_add_f32 v[22:23], v[26:27], v[22:23]
	v_mov_b32_e32 v26, v25
	v_mov_b32_e32 v27, v11
	v_pk_mul_f32 v[24:25], v[12:13], v[28:29] op_sel_hi:[1,0] neg_lo:[0,1] neg_hi:[0,1]
	v_pk_add_f32 v[34:35], v[20:21], v[22:23]
	v_pk_fma_f32 v[26:27], v[26:27], v[28:29], v[24:25] op_sel_hi:[1,0,1] neg_lo:[0,1,0] neg_hi:[0,1,0]
	v_pk_add_f32 v[24:25], v[20:21], v[22:23] neg_lo:[0,1] neg_hi:[0,1]
	v_mov_b32_e32 v43, v11
	v_pk_add_f32 v[20:21], v[24:25], 0 neg_lo:[1,1] neg_hi:[1,1]
	v_mov_b32_e32 v78, v11
	v_mov_b32_e32 v90, v24
	v_mov_b32_e32 v20, v11
	v_pk_add_f32 v[48:49], v[90:91], v[20:21]
	v_pk_add_f32 v[24:25], v[90:91], v[20:21] neg_lo:[0,1] neg_hi:[0,1]
	v_pk_add_f32 v[20:21], v[42:43], v[78:79]
	v_pk_add_f32 v[22:23], v[42:43], v[78:79] neg_lo:[0,1] neg_hi:[0,1]
	v_pk_add_f32 v[42:43], v[30:31], v[26:27]
	v_pk_add_f32 v[26:27], v[30:31], v[26:27] neg_lo:[0,1] neg_hi:[0,1]
	v_mov_b32_e32 v47, v11
	v_mov_b32_e32 v66, v11
	v_xor_b32_e32 v79, 0x80000000, v26
	v_mov_b32_e32 v78, v27
	v_pk_add_f32 v[26:27], v[62:63], v[68:69]
	v_pk_add_f32 v[62:63], v[62:63], v[68:69] neg_lo:[0,1] neg_hi:[0,1]
	v_pk_add_f32 v[90:91], v[20:21], v[42:43]
	v_pk_add_f32 v[30:31], v[20:21], v[42:43] neg_lo:[0,1] neg_hi:[0,1]
	v_pk_add_f32 v[42:43], v[22:23], v[78:79]
	v_pk_add_f32 v[20:21], v[22:23], v[78:79] neg_lo:[0,1] neg_hi:[0,1]
	v_pk_add_f32 v[22:23], v[46:47], v[66:67]
	v_pk_add_f32 v[46:47], v[46:47], v[66:67] neg_lo:[0,1] neg_hi:[0,1]
	v_pk_mul_f32 v[66:67], v[28:29], v[62:63] op_sel:[0,1] op_sel_hi:[0,0] neg_lo:[1,1] neg_hi:[1,0]
	v_pk_fma_f32 v[66:67], v[28:29], v[62:63], v[66:67] op_sel_hi:[0,1,1]
	v_pk_add_f32 v[62:63], v[64:65], v[70:71]
	v_pk_add_f32 v[64:65], v[64:65], v[70:71] neg_lo:[0,1] neg_hi:[0,1]
	v_mov_b32_e32 v80, v11
	v_xor_b32_e32 v69, 0x80000000, v64
	v_mov_b32_e32 v68, v65
	v_pk_add_f32 v[64:65], v[32:33], v[38:39]
	v_pk_add_f32 v[32:33], v[32:33], v[38:39] neg_lo:[0,1] neg_hi:[0,1]
	v_pk_add_f32 v[78:79], v[44:45], v[82:83]
	v_pk_mul_f32 v[38:39], v[28:29], v[32:33] op_sel:[0,1] op_sel_hi:[0,0] neg_lo:[1,1] neg_hi:[1,0]
	v_pk_fma_f32 v[32:33], v[28:29], v[32:33], v[38:39] op_sel_hi:[0,1,1] neg_lo:[1,0,0] neg_hi:[1,0,0]
	v_pk_add_f32 v[38:39], v[22:23], v[62:63]
	v_pk_add_f32 v[22:23], v[22:23], v[62:63] neg_lo:[0,1] neg_hi:[0,1]
	v_pk_add_f32 v[62:63], v[26:27], v[64:65]
	v_pk_add_f32 v[26:27], v[26:27], v[64:65] neg_lo:[0,1] neg_hi:[0,1]
	v_pk_add_f32 v[70:71], v[38:39], v[62:63]
	v_pk_add_f32 v[38:39], v[38:39], v[62:63] neg_lo:[0,1] neg_hi:[0,1]
	v_pk_add_f32 v[62:63], v[22:23], v[26:27] op_sel:[0,1] op_sel_hi:[1,0] neg_hi:[0,1]
	v_pk_add_f32 v[26:27], v[22:23], v[26:27] op_sel:[0,1] op_sel_hi:[1,0] neg_lo:[0,1]
	v_pk_add_f32 v[22:23], v[46:47], v[68:69]
	v_pk_add_f32 v[64:65], v[46:47], v[68:69] neg_lo:[0,1] neg_hi:[0,1]
	v_pk_add_f32 v[46:47], v[66:67], v[32:33]
	v_pk_add_f32 v[32:33], v[66:67], v[32:33] neg_lo:[0,1] neg_hi:[0,1]
	v_pk_add_f32 v[44:45], v[44:45], v[82:83] neg_lo:[0,1] neg_hi:[0,1]
	v_xor_b32_e32 v67, 0x80000000, v32
	v_mov_b32_e32 v66, v33
	v_pk_add_f32 v[68:69], v[22:23], v[46:47]
	v_pk_add_f32 v[32:33], v[22:23], v[46:47] neg_lo:[0,1] neg_hi:[0,1]
	v_pk_add_f32 v[46:47], v[64:65], v[66:67]
	v_pk_add_f32 v[22:23], v[64:65], v[66:67] neg_lo:[0,1] neg_hi:[0,1]
	v_pk_add_f32 v[64:65], v[10:11], v[80:81]
	v_pk_add_f32 v[66:67], v[10:11], v[80:81] neg_lo:[0,1] neg_hi:[0,1]
	v_pk_mul_f32 v[80:81], v[40:41], v[44:45] op_sel:[0,1] op_sel_hi:[0,0] neg_lo:[1,1] neg_hi:[1,0]
	v_pk_fma_f32 v[44:45], v[36:37], v[44:45], v[80:81] op_sel_hi:[0,1,1]
	v_pk_add_f32 v[80:81], v[50:51], v[84:85]
	v_pk_add_f32 v[50:51], v[50:51], v[84:85] neg_lo:[0,1] neg_hi:[0,1]
	v_add_f32_e32 v10, v34, v35
	v_pk_mul_f32 v[82:83], v[28:29], v[50:51] op_sel:[0,1] op_sel_hi:[0,0] neg_lo:[1,1] neg_hi:[1,0]
	v_pk_fma_f32 v[82:83], v[28:29], v[50:51], v[82:83] op_sel_hi:[0,1,1]
	v_pk_add_f32 v[50:51], v[54:55], v[86:87]
	v_pk_add_f32 v[54:55], v[54:55], v[86:87] neg_lo:[0,1] neg_hi:[0,1]
	v_pk_fma_f32 v[16:17], v[10:11], s[94:95], v[16:17] op_sel_hi:[0,1,1]
	v_pk_mul_f32 v[84:85], v[36:37], v[54:55] op_sel:[0,1] op_sel_hi:[0,0] neg_lo:[1,1] neg_hi:[1,0]
	v_pk_fma_f32 v[84:85], v[40:41], v[54:55], v[84:85] op_sel_hi:[0,1,1]
	v_pk_add_f32 v[54:55], v[56:57], v[88:89]
	v_pk_add_f32 v[56:57], v[56:57], v[88:89] neg_lo:[0,1] neg_hi:[0,1]
	v_lshl_add_u32 v13, v15, 3, 0
	v_xor_b32_e32 v87, 0x80000000, v56
	v_mov_b32_e32 v86, v57
	v_pk_add_f32 v[56:57], v[60:61], v[74:75]
	v_pk_add_f32 v[60:61], v[60:61], v[74:75] neg_lo:[0,1] neg_hi:[0,1]
	ds_write_b64 v13, v[16:17]
	v_pk_mul_f32 v[74:75], v[36:37], v[60:61] op_sel:[0,1] op_sel_hi:[0,0] neg_lo:[1,1] neg_hi:[1,0]
	v_pk_fma_f32 v[60:61], v[40:41], v[60:61], v[74:75] op_sel_hi:[0,1,1] neg_lo:[1,0,0] neg_hi:[1,0,0]
	v_pk_add_f32 v[74:75], v[58:59], v[76:77]
	v_pk_add_f32 v[58:59], v[58:59], v[76:77] neg_lo:[0,1] neg_hi:[0,1]
	v_pk_fma_f32 v[16:17], v[178:179], s[90:91], v[178:179] op_sel:[1,0,0] op_sel_hi:[0,1,1]
	v_pk_mul_f32 v[76:77], v[28:29], v[58:59] op_sel:[0,1] op_sel_hi:[0,0] neg_lo:[1,1] neg_hi:[1,0]
	v_pk_fma_f32 v[58:59], v[28:29], v[58:59], v[76:77] op_sel_hi:[0,1,1] neg_lo:[1,0,0] neg_hi:[1,0,0]
	v_pk_add_f32 v[76:77], v[52:53], v[72:73]
	v_pk_add_f32 v[52:53], v[52:53], v[72:73] neg_lo:[0,1] neg_hi:[0,1]
	s_nop 0
	v_pk_mul_f32 v[40:41], v[40:41], v[52:53] op_sel:[0,1] op_sel_hi:[0,0] neg_lo:[1,1] neg_hi:[1,0]
	v_pk_fma_f32 v[52:53], v[36:37], v[52:53], v[40:41] op_sel_hi:[0,1,1] neg_lo:[1,0,0] neg_hi:[1,0,0]
	v_pk_add_f32 v[36:37], v[64:65], v[54:55]
	v_pk_add_f32 v[64:65], v[64:65], v[54:55] neg_lo:[0,1] neg_hi:[0,1]
	v_pk_add_f32 v[54:55], v[78:79], v[56:57] neg_lo:[0,1] neg_hi:[0,1]
	v_pk_add_f32 v[40:41], v[56:57], v[78:79]
	v_pk_mul_f32 v[56:57], v[28:29], v[54:55] op_sel:[0,1] op_sel_hi:[0,0] neg_lo:[1,1] neg_hi:[1,0]
	v_pk_add_f32 v[72:73], v[80:81], v[74:75] neg_lo:[0,1] neg_hi:[0,1]
	v_pk_fma_f32 v[56:57], v[28:29], v[54:55], v[56:57] op_sel_hi:[0,1,1]
	v_pk_add_f32 v[54:55], v[80:81], v[74:75]
	v_xor_b32_e32 v75, 0x80000000, v72
	v_mov_b32_e32 v74, v73
	v_pk_add_f32 v[72:73], v[50:51], v[76:77]
	v_pk_add_f32 v[50:51], v[50:51], v[76:77] neg_lo:[0,1] neg_hi:[0,1]
	s_nop 0
	v_pk_mul_f32 v[76:77], v[28:29], v[50:51] op_sel:[0,1] op_sel_hi:[0,0] neg_lo:[1,1] neg_hi:[1,0]
	v_pk_fma_f32 v[50:51], v[28:29], v[50:51], v[76:77] op_sel_hi:[0,1,1] neg_lo:[1,0,0] neg_hi:[1,0,0]
	v_pk_add_f32 v[76:77], v[36:37], v[54:55]
	v_pk_add_f32 v[36:37], v[36:37], v[54:55] neg_lo:[0,1] neg_hi:[0,1]
	v_pk_add_f32 v[54:55], v[40:41], v[72:73]
	v_pk_add_f32 v[40:41], v[40:41], v[72:73] neg_lo:[0,1] neg_hi:[0,1]
	v_pk_add_f32 v[78:79], v[76:77], v[54:55]
	v_pk_add_f32 v[54:55], v[76:77], v[54:55] neg_lo:[0,1] neg_hi:[0,1]
	v_pk_add_f32 v[76:77], v[36:37], v[40:41] op_sel:[0,1] op_sel_hi:[1,0] neg_hi:[0,1]
	v_pk_add_f32 v[40:41], v[36:37], v[40:41] op_sel:[0,1] op_sel_hi:[1,0] neg_lo:[0,1]
	v_pk_add_f32 v[72:73], v[56:57], v[50:51]
	v_pk_add_f32 v[50:51], v[56:57], v[50:51] neg_lo:[0,1] neg_hi:[0,1]
	v_pk_add_f32 v[36:37], v[64:65], v[74:75]
	v_pk_add_f32 v[64:65], v[64:65], v[74:75] neg_lo:[0,1] neg_hi:[0,1]
	v_xor_b32_e32 v57, 0x80000000, v50
	v_mov_b32_e32 v56, v51
	v_pk_add_f32 v[74:75], v[36:37], v[72:73]
	v_pk_add_f32 v[50:51], v[36:37], v[72:73] neg_lo:[0,1] neg_hi:[0,1]
	v_pk_add_f32 v[72:73], v[64:65], v[56:57]
	v_pk_add_f32 v[36:37], v[64:65], v[56:57] neg_lo:[0,1] neg_hi:[0,1]
	v_pk_add_f32 v[56:57], v[66:67], v[86:87]
	v_pk_add_f32 v[64:65], v[66:67], v[86:87] neg_lo:[0,1] neg_hi:[0,1]
	v_pk_add_f32 v[66:67], v[60:61], v[44:45]
	v_pk_add_f32 v[44:45], v[44:45], v[60:61] neg_lo:[0,1] neg_hi:[0,1]
	s_nop 0
	v_pk_mul_f32 v[60:61], v[28:29], v[44:45] op_sel:[0,1] op_sel_hi:[0,0] neg_lo:[1,1] neg_hi:[1,0]
	v_pk_fma_f32 v[60:61], v[28:29], v[44:45], v[60:61] op_sel_hi:[0,1,1]
	v_pk_add_f32 v[44:45], v[82:83], v[58:59]
	v_pk_add_f32 v[58:59], v[82:83], v[58:59] neg_lo:[0,1] neg_hi:[0,1]
	s_nop 0
	v_xor_b32_e32 v81, 0x80000000, v58
	v_mov_b32_e32 v80, v59
	v_pk_add_f32 v[58:59], v[84:85], v[52:53]
	v_pk_add_f32 v[52:53], v[84:85], v[52:53] neg_lo:[0,1] neg_hi:[0,1]
	s_nop 0
	v_pk_mul_f32 v[82:83], v[28:29], v[52:53] op_sel:[0,1] op_sel_hi:[0,0] neg_lo:[1,1] neg_hi:[1,0]
	v_pk_fma_f32 v[28:29], v[28:29], v[52:53], v[82:83] op_sel_hi:[0,1,1] neg_lo:[1,0,0] neg_hi:[1,0,0]
	v_pk_add_f32 v[52:53], v[56:57], v[44:45]
	v_pk_add_f32 v[44:45], v[56:57], v[44:45] neg_lo:[0,1] neg_hi:[0,1]
	v_pk_add_f32 v[56:57], v[66:67], v[58:59]
	v_pk_add_f32 v[58:59], v[66:67], v[58:59] neg_lo:[0,1] neg_hi:[0,1]
	s_nop 0
	v_pk_add_f32 v[82:83], v[44:45], v[58:59] op_sel:[0,1] op_sel_hi:[1,0] neg_hi:[0,1]
	v_pk_add_f32 v[44:45], v[44:45], v[58:59] op_sel:[0,1] op_sel_hi:[1,0] neg_lo:[0,1]
	v_pk_add_f32 v[66:67], v[60:61], v[28:29]
	v_pk_add_f32 v[28:29], v[60:61], v[28:29] neg_lo:[0,1] neg_hi:[0,1]
	v_pk_add_f32 v[58:59], v[52:53], v[56:57]
	v_pk_add_f32 v[56:57], v[52:53], v[56:57] neg_lo:[0,1] neg_hi:[0,1]
	v_pk_add_f32 v[52:53], v[64:65], v[80:81]
	v_pk_add_f32 v[64:65], v[64:65], v[80:81] neg_lo:[0,1] neg_hi:[0,1]
	v_pk_add_f32 v[80:81], v[52:53], v[66:67]
	v_pk_add_f32 v[52:53], v[52:53], v[66:67] neg_lo:[0,1] neg_hi:[0,1]
	v_pk_add_f32 v[66:67], v[64:65], v[28:29] op_sel:[0,1] op_sel_hi:[1,0] neg_hi:[0,1]
	v_pk_add_f32 v[28:29], v[64:65], v[28:29] op_sel:[0,1] op_sel_hi:[1,0] neg_lo:[0,1]
	v_pk_mul_f32 v[60:61], v[16:17], v[78:79] op_sel:[1,1] op_sel_hi:[0,1] neg_lo:[0,1]
	v_pk_fma_f32 v[60:61], v[16:17], v[78:79], v[60:61] op_sel_hi:[1,0,1]
	ds_write_b64 v13, v[60:61] offset:4224
	v_pk_mul_f32 v[60:61], v[178:179], v[16:17] op_sel:[1,1] op_sel_hi:[0,1] neg_lo:[0,1]
	v_pk_fma_f32 v[16:17], v[178:179], v[16:17], v[60:61] op_sel_hi:[1,0,1]
	s_nop 0
	v_pk_mul_f32 v[60:61], v[16:17], v[70:71] op_sel:[1,1] op_sel_hi:[0,1] neg_lo:[0,1]
	v_pk_fma_f32 v[60:61], v[16:17], v[70:71], v[60:61] op_sel_hi:[1,0,1]
	ds_write_b64 v13, v[60:61] offset:8448
	v_pk_mul_f32 v[60:61], v[178:179], v[16:17] op_sel:[1,1] op_sel_hi:[0,1] neg_lo:[0,1]
	v_pk_fma_f32 v[16:17], v[178:179], v[16:17], v[60:61] op_sel_hi:[1,0,1]
	s_nop 0
	v_pk_mul_f32 v[60:61], v[16:17], v[58:59] op_sel:[1,1] op_sel_hi:[0,1] neg_lo:[0,1]
	v_pk_fma_f32 v[58:59], v[16:17], v[58:59], v[60:61] op_sel_hi:[1,0,1]
	ds_write_b64 v13, v[58:59] offset:12672
	v_pk_mul_f32 v[58:59], v[178:179], v[16:17] op_sel:[1,1] op_sel_hi:[0,1] neg_lo:[0,1]
	v_pk_fma_f32 v[16:17], v[178:179], v[16:17], v[58:59] op_sel_hi:[1,0,1]
	s_nop 0
	v_pk_mul_f32 v[58:59], v[90:91], v[16:17] op_sel:[1,1] op_sel_hi:[1,0] neg_lo:[1,0]
	s_nop 0
	v_pk_fma_f32 v[58:59], v[90:91], v[16:17], v[58:59] op_sel_hi:[0,1,1]
	ds_write_b64 v13, v[58:59] offset:16896
	v_pk_mul_f32 v[58:59], v[178:179], v[16:17] op_sel:[1,1] op_sel_hi:[0,1] neg_lo:[0,1]
	v_pk_fma_f32 v[16:17], v[178:179], v[16:17], v[58:59] op_sel_hi:[1,0,1]
	s_nop 0
	v_pk_mul_f32 v[58:59], v[16:17], v[74:75] op_sel:[1,1] op_sel_hi:[0,1] neg_lo:[0,1]
	v_pk_fma_f32 v[58:59], v[16:17], v[74:75], v[58:59] op_sel_hi:[1,0,1]
	ds_write_b64 v13, v[58:59] offset:21120
	v_pk_mul_f32 v[58:59], v[178:179], v[16:17] op_sel:[1,1] op_sel_hi:[0,1] neg_lo:[0,1]
	v_pk_fma_f32 v[16:17], v[178:179], v[16:17], v[58:59] op_sel_hi:[1,0,1]
	s_nop 0
	v_pk_mul_f32 v[58:59], v[68:69], v[16:17] op_sel:[1,1] op_sel_hi:[1,0] neg_lo:[1,0]
	s_nop 0
	v_pk_fma_f32 v[58:59], v[68:69], v[16:17], v[58:59] op_sel_hi:[0,1,1]
	ds_write_b64 v13, v[58:59] offset:25344
	v_pk_mul_f32 v[58:59], v[178:179], v[16:17] op_sel:[1,1] op_sel_hi:[0,1] neg_lo:[0,1]
	v_pk_fma_f32 v[16:17], v[178:179], v[16:17], v[58:59] op_sel_hi:[1,0,1]
	s_nop 0
	v_pk_mul_f32 v[58:59], v[80:81], v[16:17] op_sel:[1,1] op_sel_hi:[1,0] neg_lo:[1,0]
	s_nop 0
	v_pk_fma_f32 v[58:59], v[80:81], v[16:17], v[58:59] op_sel_hi:[0,1,1]
	ds_write_b64 v13, v[58:59] offset:29568
	v_pk_mul_f32 v[58:59], v[178:179], v[16:17] op_sel:[1,1] op_sel_hi:[0,1] neg_lo:[0,1]
	v_pk_fma_f32 v[16:17], v[178:179], v[16:17], v[58:59] op_sel_hi:[1,0,1]
	s_nop 0
	v_pk_mul_f32 v[58:59], v[48:49], v[16:17] op_sel:[1,1] op_sel_hi:[1,0] neg_lo:[1,0]
	s_nop 0
	v_pk_fma_f32 v[48:49], v[48:49], v[16:17], v[58:59] op_sel_hi:[0,1,1]
	ds_write_b64 v13, v[48:49] offset:33792
	v_pk_mul_f32 v[48:49], v[178:179], v[16:17] op_sel:[1,1] op_sel_hi:[0,1] neg_lo:[0,1]
	v_pk_fma_f32 v[16:17], v[178:179], v[16:17], v[48:49] op_sel_hi:[1,0,1]
	s_nop 0
	v_pk_mul_f32 v[48:49], v[76:77], v[16:17] op_sel:[1,1] op_sel_hi:[1,0] neg_lo:[1,0]
	s_nop 0
	v_pk_fma_f32 v[48:49], v[76:77], v[16:17], v[48:49] op_sel_hi:[0,1,1]
	ds_write_b64 v13, v[48:49] offset:38016
	v_pk_mul_f32 v[48:49], v[178:179], v[16:17] op_sel:[1,1] op_sel_hi:[0,1] neg_lo:[0,1]
	v_pk_fma_f32 v[16:17], v[178:179], v[16:17], v[48:49] op_sel_hi:[1,0,1]
	s_nop 0
	v_pk_mul_f32 v[48:49], v[62:63], v[16:17] op_sel:[1,1] op_sel_hi:[1,0] neg_lo:[1,0]
	s_nop 0
	v_pk_fma_f32 v[48:49], v[62:63], v[16:17], v[48:49] op_sel_hi:[0,1,1]
	ds_write_b64 v13, v[48:49] offset:42240
	v_pk_mul_f32 v[48:49], v[178:179], v[16:17] op_sel:[1,1] op_sel_hi:[0,1] neg_lo:[0,1]
	v_pk_fma_f32 v[16:17], v[178:179], v[16:17], v[48:49] op_sel_hi:[1,0,1]
	s_nop 0
	v_pk_mul_f32 v[48:49], v[82:83], v[16:17] op_sel:[1,1] op_sel_hi:[1,0] neg_lo:[1,0]
	s_nop 0
	v_pk_fma_f32 v[48:49], v[82:83], v[16:17], v[48:49] op_sel_hi:[0,1,1]
	ds_write_b64 v13, v[48:49] offset:46464
	v_pk_mul_f32 v[48:49], v[178:179], v[16:17] op_sel:[1,1] op_sel_hi:[0,1] neg_lo:[0,1]
	v_pk_fma_f32 v[16:17], v[178:179], v[16:17], v[48:49] op_sel_hi:[1,0,1]
	s_nop 0
	v_pk_mul_f32 v[48:49], v[42:43], v[16:17] op_sel:[1,1] op_sel_hi:[1,0] neg_lo:[1,0]
	s_nop 0
	v_pk_fma_f32 v[42:43], v[42:43], v[16:17], v[48:49] op_sel_hi:[0,1,1]
	ds_write_b64 v13, v[42:43] offset:50688
	v_pk_mul_f32 v[42:43], v[178:179], v[16:17] op_sel:[1,1] op_sel_hi:[0,1] neg_lo:[0,1]
	v_pk_fma_f32 v[16:17], v[178:179], v[16:17], v[42:43] op_sel_hi:[1,0,1]
	s_nop 0
	v_pk_mul_f32 v[42:43], v[72:73], v[16:17] op_sel:[1,1] op_sel_hi:[1,0] neg_lo:[1,0]
	s_nop 0
	v_pk_fma_f32 v[42:43], v[72:73], v[16:17], v[42:43] op_sel_hi:[0,1,1]
	ds_write_b64 v13, v[42:43] offset:54912
	v_pk_mul_f32 v[42:43], v[178:179], v[16:17] op_sel:[1,1] op_sel_hi:[0,1] neg_lo:[0,1]
	v_pk_fma_f32 v[16:17], v[178:179], v[16:17], v[42:43] op_sel_hi:[1,0,1]
	s_nop 0
	v_pk_mul_f32 v[42:43], v[46:47], v[16:17] op_sel:[1,1] op_sel_hi:[1,0] neg_lo:[1,0]
	s_nop 0
	v_pk_fma_f32 v[42:43], v[46:47], v[16:17], v[42:43] op_sel_hi:[0,1,1]
	ds_write_b64 v13, v[42:43] offset:59136
	v_pk_mul_f32 v[42:43], v[178:179], v[16:17] op_sel:[1,1] op_sel_hi:[0,1] neg_lo:[0,1]
	v_pk_fma_f32 v[16:17], v[178:179], v[16:17], v[42:43] op_sel_hi:[1,0,1]
	s_nop 0
	v_pk_mul_f32 v[42:43], v[66:67], v[16:17] op_sel:[1,1] op_sel_hi:[1,0] neg_lo:[1,0]
	s_nop 0
	v_pk_fma_f32 v[42:43], v[66:67], v[16:17], v[42:43] op_sel_hi:[0,1,1]
	ds_write_b64 v13, v[42:43] offset:63360
	v_pk_mul_f32 v[42:43], v[178:179], v[16:17] op_sel:[1,1] op_sel_hi:[0,1] neg_lo:[0,1]
	v_pk_fma_f32 v[16:17], v[178:179], v[16:17], v[42:43] op_sel_hi:[1,0,1]
	v_sub_f32_e32 v10, v34, v35
	v_pk_mul_f32 v[34:35], v[16:17], s[44:45]
	s_nop 0
	v_pk_fma_f32 v[34:35], v[10:11], v[16:17], v[34:35] op_sel:[0,0,1] op_sel_hi:[0,1,0]
	v_add_u32_e32 v10, 0x10800, v13
	ds_write_b64 v10, v[34:35]
	v_pk_mul_f32 v[34:35], v[178:179], v[16:17] op_sel:[1,1] op_sel_hi:[0,1] neg_lo:[0,1]
	v_pk_fma_f32 v[16:17], v[178:179], v[16:17], v[34:35] op_sel_hi:[1,0,1]
	s_nop 0
	v_pk_mul_f32 v[34:35], v[54:55], v[16:17] op_sel:[1,1] op_sel_hi:[1,0] neg_lo:[1,0]
	v_add_u32_e32 v10, 0x11880, v13
	v_pk_fma_f32 v[34:35], v[54:55], v[16:17], v[34:35] op_sel_hi:[0,1,1]
	ds_write_b64 v10, v[34:35]
	v_pk_mul_f32 v[34:35], v[178:179], v[16:17] op_sel:[1,1] op_sel_hi:[0,1] neg_lo:[0,1]
	v_pk_fma_f32 v[16:17], v[178:179], v[16:17], v[34:35] op_sel_hi:[1,0,1]
	s_nop 0
	v_pk_mul_f32 v[34:35], v[38:39], v[16:17] op_sel:[1,1] op_sel_hi:[1,0] neg_lo:[1,0]
	v_add_u32_e32 v10, 0x12900, v13
	v_pk_fma_f32 v[34:35], v[38:39], v[16:17], v[34:35] op_sel_hi:[0,1,1]
	ds_write_b64 v10, v[34:35]
	v_pk_mul_f32 v[34:35], v[178:179], v[16:17] op_sel:[1,1] op_sel_hi:[0,1] neg_lo:[0,1]
	v_pk_fma_f32 v[16:17], v[178:179], v[16:17], v[34:35] op_sel_hi:[1,0,1]
	s_nop 0
	v_pk_mul_f32 v[34:35], v[56:57], v[16:17] op_sel:[1,1] op_sel_hi:[1,0] neg_lo:[1,0]
	v_add_u32_e32 v10, 0x13980, v13
	v_pk_fma_f32 v[34:35], v[56:57], v[16:17], v[34:35] op_sel_hi:[0,1,1]
	ds_write_b64 v10, v[34:35]
	v_pk_mul_f32 v[34:35], v[178:179], v[16:17] op_sel:[1,1] op_sel_hi:[0,1] neg_lo:[0,1]
	v_pk_fma_f32 v[16:17], v[178:179], v[16:17], v[34:35] op_sel_hi:[1,0,1]
	s_nop 0
	v_pk_mul_f32 v[34:35], v[30:31], v[16:17] op_sel:[1,1] op_sel_hi:[1,0] neg_lo:[1,0]
	v_add_u32_e32 v10, 0x14a00, v13
	v_pk_fma_f32 v[30:31], v[30:31], v[16:17], v[34:35] op_sel_hi:[0,1,1]
	ds_write_b64 v10, v[30:31]
	v_pk_mul_f32 v[30:31], v[178:179], v[16:17] op_sel:[1,1] op_sel_hi:[0,1] neg_lo:[0,1]
	v_pk_fma_f32 v[16:17], v[178:179], v[16:17], v[30:31] op_sel_hi:[1,0,1]
	s_nop 0
	v_pk_mul_f32 v[30:31], v[50:51], v[16:17] op_sel:[1,1] op_sel_hi:[1,0] neg_lo:[1,0]
	v_add_u32_e32 v10, 0x15a80, v13
	v_pk_fma_f32 v[30:31], v[50:51], v[16:17], v[30:31] op_sel_hi:[0,1,1]
	ds_write_b64 v10, v[30:31]
	v_pk_mul_f32 v[30:31], v[178:179], v[16:17] op_sel:[1,1] op_sel_hi:[0,1] neg_lo:[0,1]
	v_pk_fma_f32 v[16:17], v[178:179], v[16:17], v[30:31] op_sel_hi:[1,0,1]
	s_nop 0
	v_pk_mul_f32 v[30:31], v[32:33], v[16:17] op_sel:[1,1] op_sel_hi:[1,0] neg_lo:[1,0]
	v_add_u32_e32 v10, 0x16b00, v13
	v_pk_fma_f32 v[30:31], v[32:33], v[16:17], v[30:31] op_sel_hi:[0,1,1]
	ds_write_b64 v10, v[30:31]
	v_pk_mul_f32 v[30:31], v[178:179], v[16:17] op_sel:[1,1] op_sel_hi:[0,1] neg_lo:[0,1]
	v_pk_fma_f32 v[16:17], v[178:179], v[16:17], v[30:31] op_sel_hi:[1,0,1]
	s_nop 0
	v_pk_mul_f32 v[30:31], v[52:53], v[16:17] op_sel:[1,1] op_sel_hi:[1,0] neg_lo:[1,0]
	v_add_u32_e32 v10, 0x17b80, v13
	v_pk_fma_f32 v[30:31], v[52:53], v[16:17], v[30:31] op_sel_hi:[0,1,1]
	ds_write_b64 v10, v[30:31]
	v_pk_mul_f32 v[30:31], v[178:179], v[16:17] op_sel:[1,1] op_sel_hi:[0,1] neg_lo:[0,1]
	v_pk_fma_f32 v[16:17], v[178:179], v[16:17], v[30:31] op_sel_hi:[1,0,1]
	s_nop 0
	v_pk_mul_f32 v[30:31], v[24:25], v[16:17] op_sel:[1,1] op_sel_hi:[1,0] neg_lo:[1,0]
	v_add_u32_e32 v10, 0x18c00, v13
	v_pk_fma_f32 v[24:25], v[24:25], v[16:17], v[30:31] op_sel_hi:[0,1,1]
	ds_write_b64 v10, v[24:25]
	v_pk_mul_f32 v[24:25], v[178:179], v[16:17] op_sel:[1,1] op_sel_hi:[0,1] neg_lo:[0,1]
	v_pk_fma_f32 v[16:17], v[178:179], v[16:17], v[24:25] op_sel_hi:[1,0,1]
	s_nop 0
	v_pk_mul_f32 v[24:25], v[40:41], v[16:17] op_sel:[1,1] op_sel_hi:[1,0] neg_lo:[1,0]
	v_add_u32_e32 v10, 0x19c80, v13
	v_pk_fma_f32 v[24:25], v[40:41], v[16:17], v[24:25] op_sel_hi:[0,1,1]
	ds_write_b64 v10, v[24:25]
	v_pk_mul_f32 v[24:25], v[178:179], v[16:17] op_sel:[1,1] op_sel_hi:[0,1] neg_lo:[0,1]
	v_pk_fma_f32 v[16:17], v[178:179], v[16:17], v[24:25] op_sel_hi:[1,0,1]
	s_nop 0
	v_pk_mul_f32 v[24:25], v[26:27], v[16:17] op_sel:[1,1] op_sel_hi:[1,0] neg_lo:[1,0]
	v_add_u32_e32 v10, 0x1ad00, v13
	v_pk_fma_f32 v[24:25], v[26:27], v[16:17], v[24:25] op_sel_hi:[0,1,1]
	ds_write_b64 v10, v[24:25]
	v_pk_mul_f32 v[24:25], v[178:179], v[16:17] op_sel:[1,1] op_sel_hi:[0,1] neg_lo:[0,1]
	v_pk_fma_f32 v[16:17], v[178:179], v[16:17], v[24:25] op_sel_hi:[1,0,1]
	s_nop 0
	v_pk_mul_f32 v[24:25], v[44:45], v[16:17] op_sel:[1,1] op_sel_hi:[1,0] neg_lo:[1,0]
	v_add_u32_e32 v10, 0x1bd80, v13
	v_pk_fma_f32 v[24:25], v[44:45], v[16:17], v[24:25] op_sel_hi:[0,1,1]
	ds_write_b64 v10, v[24:25]
	v_pk_mul_f32 v[24:25], v[178:179], v[16:17] op_sel:[1,1] op_sel_hi:[0,1] neg_lo:[0,1]
	v_pk_fma_f32 v[16:17], v[178:179], v[16:17], v[24:25] op_sel_hi:[1,0,1]
	s_nop 0
	v_pk_mul_f32 v[24:25], v[20:21], v[16:17] op_sel:[1,1] op_sel_hi:[1,0] neg_lo:[1,0]
	v_add_u32_e32 v10, 0x1ce00, v13
	v_pk_fma_f32 v[20:21], v[20:21], v[16:17], v[24:25] op_sel_hi:[0,1,1]
	ds_write_b64 v10, v[20:21]
	v_pk_mul_f32 v[20:21], v[178:179], v[16:17] op_sel:[1,1] op_sel_hi:[0,1] neg_lo:[0,1]
	v_pk_fma_f32 v[16:17], v[178:179], v[16:17], v[20:21] op_sel_hi:[1,0,1]
	s_nop 0
	v_pk_mul_f32 v[20:21], v[36:37], v[16:17] op_sel:[1,1] op_sel_hi:[1,0] neg_lo:[1,0]
	v_add_u32_e32 v10, 0x1de80, v13
	v_pk_fma_f32 v[20:21], v[36:37], v[16:17], v[20:21] op_sel_hi:[0,1,1]
	ds_write_b64 v10, v[20:21]
	v_pk_mul_f32 v[20:21], v[178:179], v[16:17] op_sel:[1,1] op_sel_hi:[0,1] neg_lo:[0,1]
	v_pk_fma_f32 v[16:17], v[178:179], v[16:17], v[20:21] op_sel_hi:[1,0,1]
	s_nop 0
	v_pk_mul_f32 v[20:21], v[22:23], v[16:17] op_sel:[1,1] op_sel_hi:[1,0] neg_lo:[1,0]
	v_add_u32_e32 v10, 0x1ef00, v13
	v_pk_fma_f32 v[20:21], v[22:23], v[16:17], v[20:21] op_sel_hi:[0,1,1]
	ds_write_b64 v10, v[20:21]
	v_pk_mul_f32 v[20:21], v[178:179], v[16:17] op_sel:[1,1] op_sel_hi:[0,1] neg_lo:[0,1]
	v_pk_fma_f32 v[16:17], v[178:179], v[16:17], v[20:21] op_sel_hi:[1,0,1]
	s_nop 0
	v_pk_mul_f32 v[18:19], v[28:29], v[16:17] op_sel:[1,1] op_sel_hi:[1,0] neg_lo:[1,0]
	v_add_u32_e32 v10, 0x1ff80, v13
	v_pk_fma_f32 v[16:17], v[28:29], v[16:17], v[18:19] op_sel_hi:[0,1,1]
	ds_write_b64 v10, v[16:17]
	v_mov_b32_e32 v10, v174
	v_mov_b32_e32 v13, v172
	s_waitcnt lgkmcnt(0)
	s_barrier
	v_mov_b32_e32 v16, v180
	v_add_u32_e32 v15, v13, v10
	v_lshl_add_u32 v75, v15, 3, 0
	v_xad_u32 v15, v13, 1, v10
	v_lshl_add_u32 v74, v15, 3, 0
	v_xad_u32 v15, v13, 2, v10
	v_lshl_add_u32 v73, v15, 3, 0
	v_xad_u32 v15, v13, 3, v10
	v_lshl_add_u32 v72, v15, 3, 0
	v_xad_u32 v15, v13, 4, v10
	v_lshl_add_u32 v71, v15, 3, 0
	v_xad_u32 v15, v13, 5, v10
	v_lshl_add_u32 v70, v15, 3, 0
	v_xad_u32 v15, v13, 6, v10
	v_lshl_add_u32 v69, v15, 3, 0
	v_xad_u32 v15, v13, 7, v10
	v_lshl_add_u32 v68, v15, 3, 0
	v_xad_u32 v15, v13, 8, v10
	v_lshl_add_u32 v15, v15, 3, 0
	v_add_u32_e32 v67, 0x800, v15
	v_xad_u32 v15, v13, 9, v10
	v_lshl_add_u32 v15, v15, 3, 0
	v_add_u32_e32 v66, 0x800, v15
	v_xad_u32 v15, v13, 10, v10
	v_lshl_add_u32 v15, v15, 3, 0
	v_add_u32_e32 v65, 0x800, v15
	v_xad_u32 v15, v13, 11, v10
	v_lshl_add_u32 v15, v15, 3, 0
	v_add_u32_e32 v64, 0x800, v15
	v_xad_u32 v15, v13, 12, v10
	v_mov_b32_e32 v17, v181
	v_lshl_add_u32 v15, v15, 3, 0
	ds_read2_b64 v[18:21], v75 offset1:16
	ds_read2_b64 v[40:43], v67 offset1:16
	v_add_u32_e32 v63, 0x800, v15
	v_xad_u32 v15, v13, 13, v10
	v_lshl_add_u32 v15, v15, 3, 0
	v_add_u32_e32 v62, 0x800, v15
	v_xad_u32 v15, v13, 14, v10
	v_xad_u32 v10, v13, 15, v10
	ds_read2_b64 v[22:25], v74 offset0:32 offset1:48
	ds_read2_b64 v[48:51], v66 offset0:32 offset1:48
	v_lshl_add_u32 v15, v15, 3, 0
	v_lshl_add_u32 v10, v10, 3, 0
	v_add_u32_e32 v15, 0x800, v15
	v_add_u32_e32 v13, 0x800, v10
	v_mov_b32_e32 v10, v1
	ds_read2_b64 v[26:29], v73 offset0:64 offset1:80
	ds_read2_b64 v[58:61], v72 offset0:96 offset1:112
	ds_read2_b64 v[76:79], v71 offset0:128 offset1:144
	ds_read2_b64 v[80:83], v70 offset0:160 offset1:176
	ds_read2_b64 v[84:87], v69 offset0:192 offset1:208
	ds_read2_b64 v[88:91], v68 offset0:224 offset1:240
	ds_read2_b64 v[54:57], v65 offset0:64 offset1:80
	ds_read2_b64 v[92:95], v64 offset0:96 offset1:112
	ds_read2_b64 v[96:99], v63 offset0:128 offset1:144
	ds_read2_b64 v[100:103], v62 offset0:160 offset1:176
	ds_read2_b64 v[104:107], v15 offset0:192 offset1:208
	ds_read2_b64 v[108:111], v13 offset0:224 offset1:240
	s_waitcnt lgkmcnt(14)
	v_pk_add_f32 v[112:113], v[18:19], v[40:41]
	v_pk_add_f32 v[40:41], v[18:19], v[40:41] neg_lo:[0,1] neg_hi:[0,1]
	v_pk_add_f32 v[18:19], v[20:21], v[42:43]
	v_pk_add_f32 v[20:21], v[20:21], v[42:43] neg_lo:[0,1] neg_hi:[0,1]
	v_mov_b32_e32 v30, v164
	v_mov_b32_e32 v32, v165
	v_mov_b32_e32 v34, v166
	v_mov_b32_e32 v10, v167
	v_mov_b32_e32 v38, v168
	v_mov_b32_e32 v36, v169
	v_mov_b32_e32 v46, v170
	v_mov_b32_e32 v31, v171
	v_pk_mul_f32 v[42:43], v[20:21], v[46:47] op_sel:[1,0] op_sel_hi:[0,0] neg_lo:[1,1] neg_hi:[0,1]
	s_nop 0
	v_pk_fma_f32 v[44:45], v[20:21], v[30:31], v[42:43] op_sel_hi:[1,0,1]
	s_waitcnt lgkmcnt(12)
	v_pk_add_f32 v[20:21], v[22:23], v[48:49]
	v_pk_add_f32 v[22:23], v[22:23], v[48:49] neg_lo:[0,1] neg_hi:[0,1]
	s_nop 0
	v_pk_mul_f32 v[42:43], v[22:23], v[36:37] op_sel:[1,0] op_sel_hi:[0,0] neg_lo:[1,1] neg_hi:[0,1]
	s_nop 0
	v_pk_fma_f32 v[48:49], v[22:23], v[32:33], v[42:43] op_sel_hi:[1,0,1]
	v_pk_add_f32 v[22:23], v[24:25], v[50:51]
	v_pk_add_f32 v[24:25], v[24:25], v[50:51] neg_lo:[0,1] neg_hi:[0,1]
	s_nop 0
	v_pk_mul_f32 v[42:43], v[24:25], v[38:39] op_sel:[1,0] op_sel_hi:[0,0] neg_lo:[1,1] neg_hi:[0,1]
	s_nop 0
	v_pk_fma_f32 v[52:53], v[24:25], v[34:35], v[42:43] op_sel_hi:[1,0,1]
	s_waitcnt lgkmcnt(5)
	v_pk_add_f32 v[24:25], v[26:27], v[54:55]
	v_pk_add_f32 v[26:27], v[26:27], v[54:55] neg_lo:[0,1] neg_hi:[0,1]
	s_nop 0
	v_pk_mul_f32 v[42:43], v[26:27], v[10:11] op_sel:[1,0] op_sel_hi:[0,0] neg_lo:[1,1] neg_hi:[0,1]
	s_nop 0
	v_pk_fma_f32 v[54:55], v[26:27], v[10:11], v[42:43] op_sel_hi:[1,0,1]
	v_pk_add_f32 v[26:27], v[28:29], v[56:57]
	v_pk_add_f32 v[28:29], v[28:29], v[56:57] neg_lo:[0,1] neg_hi:[0,1]
	s_nop 0
	v_pk_mul_f32 v[42:43], v[28:29], v[38:39] op_sel_hi:[1,0]
	s_nop 0
	v_pk_fma_f32 v[56:57], v[28:29], v[34:35], v[42:43] op_sel:[1,0,0] op_sel_hi:[0,0,1] neg_lo:[1,1,0] neg_hi:[0,1,0]
	s_waitcnt lgkmcnt(4)
	v_pk_add_f32 v[42:43], v[58:59], v[92:93] neg_lo:[0,1] neg_hi:[0,1]
	v_pk_add_f32 v[28:29], v[58:59], v[92:93]
	v_pk_mul_f32 v[50:51], v[42:43], v[36:37] op_sel_hi:[1,0]
	s_nop 0
	v_pk_fma_f32 v[58:59], v[42:43], v[32:33], v[50:51] op_sel:[1,0,0] op_sel_hi:[0,0,1] neg_lo:[1,1,0] neg_hi:[0,1,0]
	v_pk_add_f32 v[50:51], v[60:61], v[94:95] neg_lo:[0,1] neg_hi:[0,1]
	v_pk_add_f32 v[42:43], v[60:61], v[94:95]
	v_pk_mul_f32 v[60:61], v[50:51], v[46:47] op_sel_hi:[1,0]
	v_xor_b32_e32 v92, 0x80000000, v51
	v_mov_b32_e32 v93, v50
	s_waitcnt lgkmcnt(3)
	v_pk_add_f32 v[50:51], v[76:77], v[96:97]
	v_pk_add_f32 v[76:77], v[76:77], v[96:97] neg_lo:[0,1] neg_hi:[0,1]
	v_pk_fma_f32 v[60:61], v[92:93], v[30:31], v[60:61] op_sel_hi:[1,0,1] neg_lo:[0,1,0] neg_hi:[0,1,0]
	v_xor_b32_e32 v93, 0x80000000, v76
	v_mov_b32_e32 v92, v77
	v_pk_add_f32 v[76:77], v[78:79], v[98:99]
	v_pk_add_f32 v[78:79], v[78:79], v[98:99] neg_lo:[0,1] neg_hi:[0,1]
	s_nop 0
	v_pk_mul_f32 v[94:95], v[78:79], v[46:47] op_sel_hi:[1,0] neg_lo:[0,1] neg_hi:[0,1]
	s_nop 0
	v_pk_fma_f32 v[78:79], v[78:79], v[30:31], v[94:95] op_sel:[1,0,0] op_sel_hi:[0,0,1] neg_lo:[1,1,0] neg_hi:[0,1,0]
	s_waitcnt lgkmcnt(2)
	v_pk_add_f32 v[94:95], v[80:81], v[100:101]
	v_pk_add_f32 v[80:81], v[80:81], v[100:101] neg_lo:[0,1] neg_hi:[0,1]
	s_nop 0
	v_pk_mul_f32 v[96:97], v[80:81], v[36:37] op_sel_hi:[1,0] neg_lo:[0,1] neg_hi:[0,1]
	s_nop 0
	v_pk_fma_f32 v[80:81], v[80:81], v[32:33], v[96:97] op_sel:[1,0,0] op_sel_hi:[0,0,1] neg_lo:[1,1,0] neg_hi:[0,1,0]
	v_pk_add_f32 v[96:97], v[82:83], v[102:103]
	v_pk_add_f32 v[82:83], v[82:83], v[102:103] neg_lo:[0,1] neg_hi:[0,1]
	s_nop 0
	v_pk_mul_f32 v[98:99], v[82:83], v[38:39] op_sel_hi:[1,0] neg_lo:[0,1] neg_hi:[0,1]
	s_nop 0
	v_pk_fma_f32 v[82:83], v[82:83], v[34:35], v[98:99] op_sel:[1,0,0] op_sel_hi:[0,0,1] neg_lo:[1,1,0] neg_hi:[0,1,0]
	s_waitcnt lgkmcnt(1)
	v_pk_add_f32 v[98:99], v[84:85], v[104:105]
	v_pk_add_f32 v[84:85], v[84:85], v[104:105] neg_lo:[0,1] neg_hi:[0,1]
	s_nop 0
	v_pk_mul_f32 v[100:101], v[84:85], v[10:11] op_sel:[1,0] op_sel_hi:[0,0] neg_lo:[1,1] neg_hi:[0,1]
	s_nop 0
	v_pk_fma_f32 v[84:85], v[84:85], v[10:11], v[100:101] op_sel_hi:[1,0,1] neg_lo:[0,1,0] neg_hi:[0,1,0]
	v_pk_add_f32 v[100:101], v[86:87], v[106:107]
	v_pk_add_f32 v[86:87], v[86:87], v[106:107] neg_lo:[0,1] neg_hi:[0,1]
	s_nop 0
	v_pk_mul_f32 v[38:39], v[86:87], v[38:39] op_sel:[1,0] op_sel_hi:[0,0] neg_lo:[1,1] neg_hi:[0,1]
	s_nop 0
	v_pk_fma_f32 v[86:87], v[86:87], v[34:35], v[38:39] op_sel_hi:[1,0,1] neg_lo:[0,1,0] neg_hi:[0,1,0]
	s_waitcnt lgkmcnt(0)
	v_pk_add_f32 v[38:39], v[88:89], v[108:109] neg_lo:[0,1] neg_hi:[0,1]
	v_pk_add_f32 v[34:35], v[88:89], v[108:109]
	v_pk_mul_f32 v[88:89], v[38:39], v[36:37] op_sel:[1,0] op_sel_hi:[0,0] neg_lo:[1,1] neg_hi:[0,1]
	s_nop 0
	v_pk_fma_f32 v[88:89], v[38:39], v[32:33], v[88:89] op_sel_hi:[1,0,1] neg_lo:[0,1,0] neg_hi:[0,1,0]
	v_pk_add_f32 v[38:39], v[90:91], v[110:111]
	v_pk_add_f32 v[90:91], v[90:91], v[110:111] neg_lo:[0,1] neg_hi:[0,1]
	s_nop 0
	v_pk_mul_f32 v[46:47], v[90:91], v[46:47] op_sel:[1,0] op_sel_hi:[0,0] neg_lo:[1,1] neg_hi:[0,1]
	s_nop 0
	v_pk_fma_f32 v[90:91], v[90:91], v[30:31], v[46:47] op_sel_hi:[1,0,1] neg_lo:[0,1,0] neg_hi:[0,1,0]
	v_pk_add_f32 v[46:47], v[18:19], v[76:77]
	v_pk_add_f32 v[18:19], v[18:19], v[76:77] neg_lo:[0,1] neg_hi:[0,1]
	v_pk_add_f32 v[30:31], v[112:113], v[50:51]
	v_pk_mul_f32 v[76:77], v[18:19], v[36:37] op_sel:[1,0] op_sel_hi:[0,0] neg_lo:[1,1] neg_hi:[0,1]
	v_pk_add_f32 v[50:51], v[112:113], v[50:51] neg_lo:[0,1] neg_hi:[0,1]
	v_pk_fma_f32 v[76:77], v[18:19], v[32:33], v[76:77] op_sel_hi:[1,0,1]
	v_pk_add_f32 v[18:19], v[20:21], v[94:95]
	v_pk_add_f32 v[20:21], v[20:21], v[94:95] neg_lo:[0,1] neg_hi:[0,1]
	s_nop 0
	v_pk_mul_f32 v[94:95], v[20:21], v[10:11] op_sel:[1,0] op_sel_hi:[0,0] neg_lo:[1,1] neg_hi:[0,1]
	s_nop 0
	v_pk_fma_f32 v[20:21], v[20:21], v[10:11], v[94:95] op_sel_hi:[1,0,1]
	v_pk_add_f32 v[94:95], v[22:23], v[96:97]
	v_pk_add_f32 v[22:23], v[22:23], v[96:97] neg_lo:[0,1] neg_hi:[0,1]
	s_nop 0
	v_pk_mul_f32 v[96:97], v[22:23], v[36:37] op_sel_hi:[1,0]
	v_xor_b32_e32 v102, 0x80000000, v23
	v_mov_b32_e32 v103, v22
	v_pk_add_f32 v[22:23], v[24:25], v[98:99]
	v_pk_add_f32 v[24:25], v[24:25], v[98:99] neg_lo:[0,1] neg_hi:[0,1]
	v_pk_fma_f32 v[96:97], v[102:103], v[32:33], v[96:97] op_sel_hi:[1,0,1] neg_lo:[0,1,0] neg_hi:[0,1,0]
	v_xor_b32_e32 v99, 0x80000000, v24
	v_mov_b32_e32 v98, v25
	v_pk_add_f32 v[24:25], v[26:27], v[100:101]
	v_pk_add_f32 v[26:27], v[26:27], v[100:101] neg_lo:[0,1] neg_hi:[0,1]
	s_nop 0
	v_pk_mul_f32 v[100:101], v[26:27], v[36:37] op_sel_hi:[1,0] neg_lo:[0,1] neg_hi:[0,1]
	v_xor_b32_e32 v102, 0x80000000, v27
	v_mov_b32_e32 v103, v26
	v_pk_add_f32 v[26:27], v[28:29], v[34:35]
	v_pk_add_f32 v[28:29], v[28:29], v[34:35] neg_lo:[0,1] neg_hi:[0,1]
	v_pk_fma_f32 v[100:101], v[102:103], v[32:33], v[100:101] op_sel_hi:[1,0,1] neg_lo:[0,1,0] neg_hi:[0,1,0]
	v_pk_mul_f32 v[34:35], v[28:29], v[10:11] op_sel:[1,0] op_sel_hi:[0,0] neg_lo:[1,1] neg_hi:[0,1]
	v_pk_add_f32 v[102:103], v[30:31], v[22:23] neg_lo:[0,1] neg_hi:[0,1]
	v_pk_fma_f32 v[28:29], v[28:29], v[10:11], v[34:35] op_sel_hi:[1,0,1] neg_lo:[0,1,0] neg_hi:[0,1,0]
	v_pk_add_f32 v[34:35], v[42:43], v[38:39]
	v_pk_add_f32 v[38:39], v[42:43], v[38:39] neg_lo:[0,1] neg_hi:[0,1]
	s_nop 0
	v_pk_mul_f32 v[42:43], v[38:39], v[36:37] op_sel:[1,0] op_sel_hi:[0,0] neg_lo:[1,1] neg_hi:[0,1]
	s_nop 0
	v_pk_fma_f32 v[42:43], v[38:39], v[32:33], v[42:43] op_sel_hi:[1,0,1] neg_lo:[0,1,0] neg_hi:[0,1,0]
	v_pk_add_f32 v[38:39], v[30:31], v[22:23]
	v_pk_add_f32 v[22:23], v[46:47], v[24:25]
	v_pk_add_f32 v[24:25], v[46:47], v[24:25] neg_lo:[0,1] neg_hi:[0,1]
	s_nop 0
	v_pk_mul_f32 v[30:31], v[24:25], v[10:11] op_sel:[1,0] op_sel_hi:[0,0] neg_lo:[1,1] neg_hi:[0,1]
	s_nop 0
	v_pk_fma_f32 v[24:25], v[24:25], v[10:11], v[30:31] op_sel_hi:[1,0,1]
	v_pk_add_f32 v[30:31], v[18:19], v[26:27]
	v_pk_add_f32 v[18:19], v[18:19], v[26:27] neg_lo:[0,1] neg_hi:[0,1]
	s_nop 0
	v_xor_b32_e32 v27, 0x80000000, v18
	v_mov_b32_e32 v26, v19
	v_pk_add_f32 v[18:19], v[94:95], v[34:35]
	v_pk_add_f32 v[34:35], v[94:95], v[34:35] neg_lo:[0,1] neg_hi:[0,1]
	s_nop 0
	v_pk_mul_f32 v[46:47], v[34:35], v[10:11] op_sel:[1,0] op_sel_hi:[0,0] neg_lo:[1,1] neg_hi:[0,1]
	s_nop 0
	v_pk_fma_f32 v[34:35], v[34:35], v[10:11], v[46:47] op_sel_hi:[1,0,1] neg_lo:[0,1,0] neg_hi:[0,1,0]
	v_pk_add_f32 v[46:47], v[38:39], v[30:31]
	v_pk_add_f32 v[38:39], v[38:39], v[30:31] neg_lo:[0,1] neg_hi:[0,1]
	v_pk_add_f32 v[30:31], v[22:23], v[18:19]
	v_pk_add_f32 v[18:19], v[22:23], v[18:19] neg_lo:[0,1] neg_hi:[0,1]
	v_pk_add_f32 v[94:95], v[46:47], v[30:31]
	v_xor_b32_e32 v23, 0x80000000, v18
	v_mov_b32_e32 v22, v19
	v_pk_add_f32 v[18:19], v[102:103], v[26:27]
	v_pk_add_f32 v[102:103], v[102:103], v[26:27] neg_lo:[0,1] neg_hi:[0,1]
	v_pk_add_f32 v[26:27], v[24:25], v[34:35]
	v_pk_add_f32 v[24:25], v[24:25], v[34:35] neg_lo:[0,1] neg_hi:[0,1]
	v_pk_add_f32 v[30:31], v[46:47], v[30:31] neg_lo:[0,1] neg_hi:[0,1]
	v_xor_b32_e32 v35, 0x80000000, v24
	v_mov_b32_e32 v34, v25
	v_pk_add_f32 v[24:25], v[50:51], v[98:99]
	v_pk_add_f32 v[98:99], v[50:51], v[98:99] neg_lo:[0,1] neg_hi:[0,1]
	v_pk_add_f32 v[50:51], v[76:77], v[100:101] neg_lo:[0,1] neg_hi:[0,1]
	v_pk_add_f32 v[46:47], v[38:39], v[22:23]
	v_pk_add_f32 v[22:23], v[38:39], v[22:23] neg_lo:[0,1] neg_hi:[0,1]
	v_pk_add_f32 v[104:105], v[18:19], v[26:27]
	v_pk_add_f32 v[26:27], v[18:19], v[26:27] neg_lo:[0,1] neg_hi:[0,1]
	v_pk_add_f32 v[38:39], v[102:103], v[34:35]
	v_pk_add_f32 v[18:19], v[102:103], v[34:35] neg_lo:[0,1] neg_hi:[0,1]
	v_pk_add_f32 v[34:35], v[76:77], v[100:101]
	v_pk_mul_f32 v[76:77], v[10:11], v[50:51] op_sel:[0,1] op_sel_hi:[0,0] neg_lo:[1,1] neg_hi:[1,0]
	v_pk_fma_f32 v[76:77], v[10:11], v[50:51], v[76:77] op_sel_hi:[0,1,1]
	v_pk_add_f32 v[50:51], v[20:21], v[28:29]
	v_pk_add_f32 v[20:21], v[20:21], v[28:29] neg_lo:[0,1] neg_hi:[0,1]
	s_nop 0
	v_xor_b32_e32 v29, 0x80000000, v20
	v_mov_b32_e32 v28, v21
	v_pk_add_f32 v[20:21], v[96:97], v[42:43]
	v_pk_add_f32 v[42:43], v[96:97], v[42:43] neg_lo:[0,1] neg_hi:[0,1]
	s_nop 0
	v_pk_mul_f32 v[96:97], v[10:11], v[42:43] op_sel:[0,1] op_sel_hi:[0,0] neg_lo:[1,1] neg_hi:[1,0]
	v_pk_fma_f32 v[42:43], v[10:11], v[42:43], v[96:97] op_sel_hi:[0,1,1] neg_lo:[1,0,0] neg_hi:[1,0,0]
	v_pk_add_f32 v[96:97], v[24:25], v[50:51]
	v_pk_add_f32 v[24:25], v[24:25], v[50:51] neg_lo:[0,1] neg_hi:[0,1]
	v_pk_add_f32 v[50:51], v[34:35], v[20:21]
	v_pk_add_f32 v[20:21], v[34:35], v[20:21] neg_lo:[0,1] neg_hi:[0,1]
	v_pk_add_f32 v[102:103], v[96:97], v[50:51]
	v_xor_b32_e32 v101, 0x80000000, v20
	v_mov_b32_e32 v100, v21
	v_pk_add_f32 v[34:35], v[96:97], v[50:51] neg_lo:[0,1] neg_hi:[0,1]
	v_pk_add_f32 v[20:21], v[98:99], v[28:29]
	v_pk_add_f32 v[96:97], v[98:99], v[28:29] neg_lo:[0,1] neg_hi:[0,1]
	v_pk_add_f32 v[28:29], v[76:77], v[42:43]
	v_pk_add_f32 v[42:43], v[76:77], v[42:43] neg_lo:[0,1] neg_hi:[0,1]
	v_pk_add_f32 v[98:99], v[20:21], v[28:29]
	v_xor_b32_e32 v77, 0x80000000, v42
	v_mov_b32_e32 v76, v43
	v_pk_add_f32 v[28:29], v[20:21], v[28:29] neg_lo:[0,1] neg_hi:[0,1]
	v_pk_add_f32 v[42:43], v[96:97], v[76:77]
	v_pk_add_f32 v[20:21], v[96:97], v[76:77] neg_lo:[0,1] neg_hi:[0,1]
	v_pk_add_f32 v[76:77], v[40:41], v[92:93]
	v_pk_add_f32 v[92:93], v[40:41], v[92:93] neg_lo:[0,1] neg_hi:[0,1]
	v_pk_add_f32 v[40:41], v[44:45], v[78:79]
	v_pk_add_f32 v[44:45], v[44:45], v[78:79] neg_lo:[0,1] neg_hi:[0,1]
	v_pk_add_f32 v[50:51], v[24:25], v[100:101]
	v_pk_mul_f32 v[78:79], v[36:37], v[44:45] op_sel:[0,1] op_sel_hi:[0,0] neg_lo:[1,1] neg_hi:[1,0]
	v_pk_fma_f32 v[44:45], v[32:33], v[44:45], v[78:79] op_sel_hi:[0,1,1]
	v_pk_add_f32 v[78:79], v[48:49], v[80:81]
	v_pk_add_f32 v[48:49], v[48:49], v[80:81] neg_lo:[0,1] neg_hi:[0,1]
	v_pk_add_f32 v[24:25], v[24:25], v[100:101] neg_lo:[0,1] neg_hi:[0,1]
	v_pk_mul_f32 v[80:81], v[10:11], v[48:49] op_sel:[0,1] op_sel_hi:[0,0] neg_lo:[1,1] neg_hi:[1,0]
	v_pk_fma_f32 v[80:81], v[10:11], v[48:49], v[80:81] op_sel_hi:[0,1,1]
	v_pk_add_f32 v[48:49], v[52:53], v[82:83]
	v_pk_add_f32 v[52:53], v[52:53], v[82:83] neg_lo:[0,1] neg_hi:[0,1]
	s_nop 0
	v_pk_mul_f32 v[82:83], v[32:33], v[52:53] op_sel:[0,1] op_sel_hi:[0,0] neg_lo:[1,1] neg_hi:[1,0]
	v_pk_fma_f32 v[52:53], v[36:37], v[52:53], v[82:83] op_sel_hi:[0,1,1]
	v_pk_add_f32 v[82:83], v[54:55], v[84:85]
	v_pk_add_f32 v[54:55], v[54:55], v[84:85] neg_lo:[0,1] neg_hi:[0,1]
	s_nop 0
	v_xor_b32_e32 v85, 0x80000000, v54
	v_mov_b32_e32 v84, v55
	v_pk_add_f32 v[54:55], v[56:57], v[86:87]
	v_pk_add_f32 v[56:57], v[56:57], v[86:87] neg_lo:[0,1] neg_hi:[0,1]
	s_nop 0
	v_pk_mul_f32 v[86:87], v[32:33], v[56:57] op_sel:[0,1] op_sel_hi:[0,0] neg_lo:[1,1] neg_hi:[1,0]
	v_pk_fma_f32 v[56:57], v[36:37], v[56:57], v[86:87] op_sel_hi:[0,1,1] neg_lo:[1,0,0] neg_hi:[1,0,0]
	v_pk_add_f32 v[86:87], v[58:59], v[88:89]
	v_pk_add_f32 v[58:59], v[58:59], v[88:89] neg_lo:[0,1] neg_hi:[0,1]
	s_nop 0
	v_pk_mul_f32 v[88:89], v[10:11], v[58:59] op_sel:[0,1] op_sel_hi:[0,0] neg_lo:[1,1] neg_hi:[1,0]
	v_pk_fma_f32 v[58:59], v[10:11], v[58:59], v[88:89] op_sel_hi:[0,1,1] neg_lo:[1,0,0] neg_hi:[1,0,0]
	v_pk_add_f32 v[88:89], v[60:61], v[90:91]
	v_pk_add_f32 v[60:61], v[60:61], v[90:91] neg_lo:[0,1] neg_hi:[0,1]
	s_nop 0
	v_pk_mul_f32 v[36:37], v[36:37], v[60:61] op_sel:[0,1] op_sel_hi:[0,0] neg_lo:[1,1] neg_hi:[1,0]
	v_pk_fma_f32 v[36:37], v[32:33], v[60:61], v[36:37] op_sel_hi:[0,1,1] neg_lo:[1,0,0] neg_hi:[1,0,0]
	v_pk_add_f32 v[32:33], v[76:77], v[82:83]
	v_pk_add_f32 v[60:61], v[76:77], v[82:83] neg_lo:[0,1] neg_hi:[0,1]
	v_pk_add_f32 v[76:77], v[54:55], v[40:41]
	v_pk_add_f32 v[40:41], v[40:41], v[54:55] neg_lo:[0,1] neg_hi:[0,1]
	s_nop 0
	v_pk_mul_f32 v[54:55], v[10:11], v[40:41] op_sel:[0,1] op_sel_hi:[0,0] neg_lo:[1,1] neg_hi:[1,0]
	v_pk_fma_f32 v[54:55], v[10:11], v[40:41], v[54:55] op_sel_hi:[0,1,1]
	v_pk_add_f32 v[40:41], v[78:79], v[86:87]
	v_pk_add_f32 v[78:79], v[78:79], v[86:87] neg_lo:[0,1] neg_hi:[0,1]
	s_nop 0
	v_xor_b32_e32 v83, 0x80000000, v78
	v_mov_b32_e32 v82, v79
	v_pk_add_f32 v[78:79], v[48:49], v[88:89]
	v_pk_add_f32 v[48:49], v[48:49], v[88:89] neg_lo:[0,1] neg_hi:[0,1]
	v_pk_add_f32 v[88:89], v[76:77], v[78:79]
	v_pk_mul_f32 v[86:87], v[10:11], v[48:49] op_sel:[0,1] op_sel_hi:[0,0] neg_lo:[1,1] neg_hi:[1,0]
	v_pk_fma_f32 v[48:49], v[10:11], v[48:49], v[86:87] op_sel_hi:[0,1,1] neg_lo:[1,0,0] neg_hi:[1,0,0]
	v_pk_add_f32 v[86:87], v[32:33], v[40:41]
	v_pk_add_f32 v[32:33], v[32:33], v[40:41] neg_lo:[0,1] neg_hi:[0,1]
	v_pk_add_f32 v[40:41], v[76:77], v[78:79] neg_lo:[0,1] neg_hi:[0,1]
	v_pk_add_f32 v[78:79], v[86:87], v[88:89] neg_lo:[0,1] neg_hi:[0,1]
	v_pk_add_f32 v[90:91], v[32:33], v[40:41] op_sel:[0,1] op_sel_hi:[1,0] neg_hi:[0,1]
	v_pk_add_f32 v[40:41], v[32:33], v[40:41] op_sel:[0,1] op_sel_hi:[1,0] neg_lo:[0,1]
	v_pk_add_f32 v[76:77], v[54:55], v[48:49]
	v_pk_add_f32 v[48:49], v[54:55], v[48:49] neg_lo:[0,1] neg_hi:[0,1]
	v_pk_add_f32 v[32:33], v[60:61], v[82:83]
	v_pk_add_f32 v[60:61], v[60:61], v[82:83] neg_lo:[0,1] neg_hi:[0,1]
	v_xor_b32_e32 v55, 0x80000000, v48
	v_mov_b32_e32 v54, v49
	v_pk_add_f32 v[82:83], v[32:33], v[76:77]
	v_pk_add_f32 v[48:49], v[32:33], v[76:77] neg_lo:[0,1] neg_hi:[0,1]
	v_pk_add_f32 v[76:77], v[60:61], v[54:55]
	v_pk_add_f32 v[32:33], v[60:61], v[54:55] neg_lo:[0,1] neg_hi:[0,1]
	v_pk_add_f32 v[54:55], v[92:93], v[84:85]
	v_pk_add_f32 v[60:61], v[92:93], v[84:85] neg_lo:[0,1] neg_hi:[0,1]
	v_pk_add_f32 v[84:85], v[56:57], v[44:45]
	v_pk_add_f32 v[44:45], v[44:45], v[56:57] neg_lo:[0,1] neg_hi:[0,1]
	v_pk_add_f32 v[86:87], v[86:87], v[88:89]
	v_pk_mul_f32 v[56:57], v[10:11], v[44:45] op_sel:[0,1] op_sel_hi:[0,0] neg_lo:[1,1] neg_hi:[1,0]
	v_pk_fma_f32 v[56:57], v[10:11], v[44:45], v[56:57] op_sel_hi:[0,1,1]
	v_pk_add_f32 v[44:45], v[80:81], v[58:59]
	v_pk_add_f32 v[58:59], v[80:81], v[58:59] neg_lo:[0,1] neg_hi:[0,1]
	s_nop 0
	v_xor_b32_e32 v81, 0x80000000, v58
	v_mov_b32_e32 v80, v59
	v_pk_add_f32 v[58:59], v[52:53], v[36:37]
	v_pk_add_f32 v[36:37], v[52:53], v[36:37] neg_lo:[0,1] neg_hi:[0,1]
	s_nop 0
	v_pk_mul_f32 v[52:53], v[10:11], v[36:37] op_sel:[0,1] op_sel_hi:[0,0] neg_lo:[1,1] neg_hi:[1,0]
	v_pk_fma_f32 v[36:37], v[10:11], v[36:37], v[52:53] op_sel_hi:[0,1,1] neg_lo:[1,0,0] neg_hi:[1,0,0]
	v_pk_add_f32 v[52:53], v[54:55], v[44:45]
	v_pk_add_f32 v[44:45], v[54:55], v[44:45] neg_lo:[0,1] neg_hi:[0,1]
	v_pk_add_f32 v[54:55], v[84:85], v[58:59]
	v_pk_add_f32 v[58:59], v[84:85], v[58:59] neg_lo:[0,1] neg_hi:[0,1]
	s_nop 0
	v_xor_b32_e32 v85, 0x80000000, v58
	v_mov_b32_e32 v84, v59
	v_pk_add_f32 v[58:59], v[52:53], v[54:55]
	v_pk_add_f32 v[52:53], v[52:53], v[54:55] neg_lo:[0,1] neg_hi:[0,1]
	v_pk_add_f32 v[54:55], v[44:45], v[84:85]
	v_pk_add_f32 v[44:45], v[44:45], v[84:85] neg_lo:[0,1] neg_hi:[0,1]
	v_pk_add_f32 v[84:85], v[60:61], v[80:81]
	v_pk_add_f32 v[60:61], v[60:61], v[80:81] neg_lo:[0,1] neg_hi:[0,1]
	v_pk_add_f32 v[80:81], v[56:57], v[36:37]
	v_pk_add_f32 v[36:37], v[56:57], v[36:37] neg_lo:[0,1] neg_hi:[0,1]
	v_pk_add_f32 v[92:93], v[84:85], v[80:81]
	v_pk_add_f32 v[80:81], v[84:85], v[80:81] neg_lo:[0,1] neg_hi:[0,1]
	v_pk_add_f32 v[84:85], v[60:61], v[36:37] op_sel:[0,1] op_sel_hi:[1,0] neg_hi:[0,1]
	v_pk_add_f32 v[36:37], v[60:61], v[36:37] op_sel:[0,1] op_sel_hi:[1,0] neg_lo:[0,1]
	v_pk_fma_f32 v[60:61], v[16:17], s[90:91], v[16:17] op_sel:[1,0,0] op_sel_hi:[0,1,1]
	v_pk_mul_f32 v[56:57], v[94:95], s[14:15] op_sel:[1,0] neg_lo:[1,0]
	v_pk_mul_f32 v[88:89], v[60:61], v[86:87] op_sel:[1,1] op_sel_hi:[0,1] neg_lo:[0,1]
	v_pk_fma_f32 v[56:57], v[94:95], s[94:95], v[56:57] op_sel_hi:[0,1,1]
	v_pk_fma_f32 v[86:87], v[60:61], v[86:87], v[88:89] op_sel_hi:[1,0,1]
	ds_write2_b64 v75, v[56:57], v[86:87] offset1:16
	v_pk_mul_f32 v[56:57], v[16:17], v[60:61] op_sel:[1,1] op_sel_hi:[0,1] neg_lo:[0,1]
	v_pk_fma_f32 v[56:57], v[16:17], v[60:61], v[56:57] op_sel_hi:[1,0,1]
	s_nop 0
	v_pk_mul_f32 v[60:61], v[56:57], v[102:103] op_sel:[1,1] op_sel_hi:[0,1] neg_lo:[0,1]
	v_pk_mul_f32 v[86:87], v[16:17], v[56:57] op_sel:[1,1] op_sel_hi:[0,1] neg_lo:[0,1]
	v_pk_fma_f32 v[60:61], v[56:57], v[102:103], v[60:61] op_sel_hi:[1,0,1]
	v_pk_fma_f32 v[56:57], v[16:17], v[56:57], v[86:87] op_sel_hi:[1,0,1]
	s_nop 0
	v_pk_mul_f32 v[86:87], v[56:57], v[58:59] op_sel:[1,1] op_sel_hi:[0,1] neg_lo:[0,1]
	v_pk_fma_f32 v[58:59], v[56:57], v[58:59], v[86:87] op_sel_hi:[1,0,1]
	ds_write2_b64 v74, v[60:61], v[58:59] offset0:32 offset1:48
	v_pk_mul_f32 v[58:59], v[16:17], v[56:57] op_sel:[1,1] op_sel_hi:[0,1] neg_lo:[0,1]
	v_pk_fma_f32 v[56:57], v[16:17], v[56:57], v[58:59] op_sel_hi:[1,0,1]
	s_nop 0
	v_pk_mul_f32 v[58:59], v[56:57], v[104:105] op_sel:[1,1] op_sel_hi:[0,1] neg_lo:[0,1]
	v_pk_mul_f32 v[60:61], v[16:17], v[56:57] op_sel:[1,1] op_sel_hi:[0,1] neg_lo:[0,1]
	v_pk_fma_f32 v[58:59], v[56:57], v[104:105], v[58:59] op_sel_hi:[1,0,1]
	v_pk_fma_f32 v[56:57], v[16:17], v[56:57], v[60:61] op_sel_hi:[1,0,1]
	s_nop 0
	v_pk_mul_f32 v[60:61], v[56:57], v[82:83] op_sel:[1,1] op_sel_hi:[0,1] neg_lo:[0,1]
	v_pk_fma_f32 v[60:61], v[56:57], v[82:83], v[60:61] op_sel_hi:[1,0,1]
	ds_write2_b64 v73, v[58:59], v[60:61] offset0:64 offset1:80
	v_pk_mul_f32 v[58:59], v[16:17], v[56:57] op_sel:[1,1] op_sel_hi:[0,1] neg_lo:[0,1]
	v_pk_fma_f32 v[56:57], v[16:17], v[56:57], v[58:59] op_sel_hi:[1,0,1]
	s_nop 0
	v_pk_mul_f32 v[58:59], v[56:57], v[98:99] op_sel:[1,1] op_sel_hi:[0,1] neg_lo:[0,1]
	v_pk_mul_f32 v[60:61], v[16:17], v[56:57] op_sel:[1,1] op_sel_hi:[0,1] neg_lo:[0,1]
	v_pk_fma_f32 v[58:59], v[56:57], v[98:99], v[58:59] op_sel_hi:[1,0,1]
	v_pk_fma_f32 v[56:57], v[16:17], v[56:57], v[60:61] op_sel_hi:[1,0,1]
	s_nop 0
	v_pk_mul_f32 v[60:61], v[56:57], v[92:93] op_sel:[1,1] op_sel_hi:[0,1] neg_lo:[0,1]
	v_pk_fma_f32 v[60:61], v[56:57], v[92:93], v[60:61] op_sel_hi:[1,0,1]
	ds_write2_b64 v72, v[58:59], v[60:61] offset0:96 offset1:112
	v_pk_mul_f32 v[58:59], v[16:17], v[56:57] op_sel:[1,1] op_sel_hi:[0,1] neg_lo:[0,1]
	v_pk_fma_f32 v[56:57], v[16:17], v[56:57], v[58:59] op_sel_hi:[1,0,1]
	s_nop 0
	v_pk_mul_f32 v[58:59], v[56:57], v[46:47] op_sel:[1,1] op_sel_hi:[0,1] neg_lo:[0,1]
	v_pk_fma_f32 v[46:47], v[56:57], v[46:47], v[58:59] op_sel_hi:[1,0,1]
	v_pk_mul_f32 v[58:59], v[16:17], v[56:57] op_sel:[1,1] op_sel_hi:[0,1] neg_lo:[0,1]
	v_pk_fma_f32 v[56:57], v[16:17], v[56:57], v[58:59] op_sel_hi:[1,0,1]
	s_nop 0
	v_pk_mul_f32 v[58:59], v[56:57], v[90:91] op_sel:[1,1] op_sel_hi:[0,1] neg_lo:[0,1]
	v_pk_fma_f32 v[58:59], v[56:57], v[90:91], v[58:59] op_sel_hi:[1,0,1]
	ds_write2_b64 v71, v[46:47], v[58:59] offset0:128 offset1:144
	v_pk_mul_f32 v[46:47], v[16:17], v[56:57] op_sel:[1,1] op_sel_hi:[0,1] neg_lo:[0,1]
	v_pk_fma_f32 v[46:47], v[16:17], v[56:57], v[46:47] op_sel_hi:[1,0,1]
	s_nop 0
	v_pk_mul_f32 v[56:57], v[46:47], v[50:51] op_sel:[1,1] op_sel_hi:[0,1] neg_lo:[0,1]
	v_pk_fma_f32 v[50:51], v[46:47], v[50:51], v[56:57] op_sel_hi:[1,0,1]
	v_pk_mul_f32 v[56:57], v[16:17], v[46:47] op_sel:[1,1] op_sel_hi:[0,1] neg_lo:[0,1]
	v_pk_fma_f32 v[46:47], v[16:17], v[46:47], v[56:57] op_sel_hi:[1,0,1]
	s_nop 0
	v_pk_mul_f32 v[56:57], v[46:47], v[54:55] op_sel:[1,1] op_sel_hi:[0,1] neg_lo:[0,1]
	v_pk_fma_f32 v[54:55], v[46:47], v[54:55], v[56:57] op_sel_hi:[1,0,1]
	ds_write2_b64 v70, v[50:51], v[54:55] offset0:160 offset1:176
	v_pk_mul_f32 v[50:51], v[16:17], v[46:47] op_sel:[1,1] op_sel_hi:[0,1] neg_lo:[0,1]
	v_pk_fma_f32 v[46:47], v[16:17], v[46:47], v[50:51] op_sel_hi:[1,0,1]
	s_nop 0
	v_pk_mul_f32 v[50:51], v[38:39], v[46:47] op_sel:[1,1] op_sel_hi:[1,0] neg_lo:[1,0]
	s_nop 0
	v_pk_fma_f32 v[38:39], v[38:39], v[46:47], v[50:51] op_sel_hi:[0,1,1]
	v_pk_mul_f32 v[50:51], v[16:17], v[46:47] op_sel:[1,1] op_sel_hi:[0,1] neg_lo:[0,1]
	v_pk_fma_f32 v[46:47], v[16:17], v[46:47], v[50:51] op_sel_hi:[1,0,1]
	s_nop 0
	v_pk_mul_f32 v[50:51], v[46:47], v[76:77] op_sel:[1,1] op_sel_hi:[0,1] neg_lo:[0,1]
	v_pk_fma_f32 v[50:51], v[46:47], v[76:77], v[50:51] op_sel_hi:[1,0,1]
	ds_write2_b64 v69, v[38:39], v[50:51] offset0:192 offset1:208
	v_pk_mul_f32 v[38:39], v[16:17], v[46:47] op_sel:[1,1] op_sel_hi:[0,1] neg_lo:[0,1]
	v_pk_fma_f32 v[38:39], v[16:17], v[46:47], v[38:39] op_sel_hi:[1,0,1]
	s_nop 0
	v_pk_mul_f32 v[46:47], v[42:43], v[38:39] op_sel:[1,1] op_sel_hi:[1,0] neg_lo:[1,0]
	s_nop 0
	v_pk_fma_f32 v[42:43], v[42:43], v[38:39], v[46:47] op_sel_hi:[0,1,1]
	v_pk_mul_f32 v[46:47], v[16:17], v[38:39] op_sel:[1,1] op_sel_hi:[0,1] neg_lo:[0,1]
	v_pk_fma_f32 v[38:39], v[16:17], v[38:39], v[46:47] op_sel_hi:[1,0,1]
	s_nop 0
	v_pk_mul_f32 v[46:47], v[38:39], v[84:85] op_sel:[1,1] op_sel_hi:[0,1] neg_lo:[0,1]
	v_pk_fma_f32 v[46:47], v[38:39], v[84:85], v[46:47] op_sel_hi:[1,0,1]
	ds_write2_b64 v68, v[42:43], v[46:47] offset0:224 offset1:240
	v_pk_mul_f32 v[42:43], v[16:17], v[38:39] op_sel:[1,1] op_sel_hi:[0,1] neg_lo:[0,1]
	v_pk_fma_f32 v[38:39], v[16:17], v[38:39], v[42:43] op_sel_hi:[1,0,1]
	s_nop 0
	v_pk_mul_f32 v[42:43], v[30:31], v[38:39] op_sel:[1,1] op_sel_hi:[1,0] neg_lo:[1,0]
	s_nop 0
	v_pk_fma_f32 v[30:31], v[30:31], v[38:39], v[42:43] op_sel_hi:[0,1,1]
	v_pk_mul_f32 v[42:43], v[16:17], v[38:39] op_sel:[1,1] op_sel_hi:[0,1] neg_lo:[0,1]
	v_pk_fma_f32 v[38:39], v[16:17], v[38:39], v[42:43] op_sel_hi:[1,0,1]
	s_nop 0
	v_pk_mul_f32 v[42:43], v[78:79], v[38:39] op_sel:[1,1] op_sel_hi:[1,0] neg_lo:[1,0]
	s_nop 0
	v_pk_fma_f32 v[42:43], v[78:79], v[38:39], v[42:43] op_sel_hi:[0,1,1]
	ds_write2_b64 v67, v[30:31], v[42:43] offset1:16
	v_pk_mul_f32 v[30:31], v[16:17], v[38:39] op_sel:[1,1] op_sel_hi:[0,1] neg_lo:[0,1]
	v_pk_fma_f32 v[30:31], v[16:17], v[38:39], v[30:31] op_sel_hi:[1,0,1]
	s_nop 0
	v_pk_mul_f32 v[38:39], v[34:35], v[30:31] op_sel:[1,1] op_sel_hi:[1,0] neg_lo:[1,0]
	s_nop 0
	v_pk_fma_f32 v[34:35], v[34:35], v[30:31], v[38:39] op_sel_hi:[0,1,1]
	v_pk_mul_f32 v[38:39], v[16:17], v[30:31] op_sel:[1,1] op_sel_hi:[0,1] neg_lo:[0,1]
	v_pk_fma_f32 v[30:31], v[16:17], v[30:31], v[38:39] op_sel_hi:[1,0,1]
	s_nop 0
	v_pk_mul_f32 v[38:39], v[52:53], v[30:31] op_sel:[1,1] op_sel_hi:[1,0] neg_lo:[1,0]
	s_nop 0
	v_pk_fma_f32 v[38:39], v[52:53], v[30:31], v[38:39] op_sel_hi:[0,1,1]
	ds_write2_b64 v66, v[34:35], v[38:39] offset0:32 offset1:48
	v_pk_mul_f32 v[34:35], v[16:17], v[30:31] op_sel:[1,1] op_sel_hi:[0,1] neg_lo:[0,1]
	v_pk_fma_f32 v[30:31], v[16:17], v[30:31], v[34:35] op_sel_hi:[1,0,1]
	s_nop 0
	v_pk_mul_f32 v[34:35], v[26:27], v[30:31] op_sel:[1,1] op_sel_hi:[1,0] neg_lo:[1,0]
	s_nop 0
	v_pk_fma_f32 v[26:27], v[26:27], v[30:31], v[34:35] op_sel_hi:[0,1,1]
	v_pk_mul_f32 v[34:35], v[16:17], v[30:31] op_sel:[1,1] op_sel_hi:[0,1] neg_lo:[0,1]
	v_pk_fma_f32 v[30:31], v[16:17], v[30:31], v[34:35] op_sel_hi:[1,0,1]
	s_nop 0
	v_pk_mul_f32 v[34:35], v[48:49], v[30:31] op_sel:[1,1] op_sel_hi:[1,0] neg_lo:[1,0]
	s_nop 0
	v_pk_fma_f32 v[34:35], v[48:49], v[30:31], v[34:35] op_sel_hi:[0,1,1]
	ds_write2_b64 v65, v[26:27], v[34:35] offset0:64 offset1:80
	v_pk_mul_f32 v[26:27], v[16:17], v[30:31] op_sel:[1,1] op_sel_hi:[0,1] neg_lo:[0,1]
	v_pk_fma_f32 v[26:27], v[16:17], v[30:31], v[26:27] op_sel_hi:[1,0,1]
	s_nop 0
	v_pk_mul_f32 v[30:31], v[28:29], v[26:27] op_sel:[1,1] op_sel_hi:[1,0] neg_lo:[1,0]
	s_nop 0
	v_pk_fma_f32 v[28:29], v[28:29], v[26:27], v[30:31] op_sel_hi:[0,1,1]
	v_pk_mul_f32 v[30:31], v[16:17], v[26:27] op_sel:[1,1] op_sel_hi:[0,1] neg_lo:[0,1]
	v_pk_fma_f32 v[26:27], v[16:17], v[26:27], v[30:31] op_sel_hi:[1,0,1]
	s_nop 0
	v_pk_mul_f32 v[30:31], v[80:81], v[26:27] op_sel:[1,1] op_sel_hi:[1,0] neg_lo:[1,0]
	s_nop 0
	v_pk_fma_f32 v[30:31], v[80:81], v[26:27], v[30:31] op_sel_hi:[0,1,1]
	ds_write2_b64 v64, v[28:29], v[30:31] offset0:96 offset1:112
	v_pk_mul_f32 v[28:29], v[16:17], v[26:27] op_sel:[1,1] op_sel_hi:[0,1] neg_lo:[0,1]
	v_pk_fma_f32 v[26:27], v[16:17], v[26:27], v[28:29] op_sel_hi:[1,0,1]
	s_nop 0
	v_pk_mul_f32 v[28:29], v[22:23], v[26:27] op_sel:[1,1] op_sel_hi:[1,0] neg_lo:[1,0]
	s_nop 0
	v_pk_fma_f32 v[22:23], v[22:23], v[26:27], v[28:29] op_sel_hi:[0,1,1]
	v_pk_mul_f32 v[28:29], v[16:17], v[26:27] op_sel:[1,1] op_sel_hi:[0,1] neg_lo:[0,1]
	v_pk_fma_f32 v[26:27], v[16:17], v[26:27], v[28:29] op_sel_hi:[1,0,1]
	s_nop 0
	v_pk_mul_f32 v[28:29], v[40:41], v[26:27] op_sel:[1,1] op_sel_hi:[1,0] neg_lo:[1,0]
	s_nop 0
	v_pk_fma_f32 v[28:29], v[40:41], v[26:27], v[28:29] op_sel_hi:[0,1,1]
	ds_write2_b64 v63, v[22:23], v[28:29] offset0:128 offset1:144
	v_pk_mul_f32 v[22:23], v[16:17], v[26:27] op_sel:[1,1] op_sel_hi:[0,1] neg_lo:[0,1]
	v_pk_fma_f32 v[22:23], v[16:17], v[26:27], v[22:23] op_sel_hi:[1,0,1]
	s_nop 0
	v_pk_mul_f32 v[26:27], v[24:25], v[22:23] op_sel:[1,1] op_sel_hi:[1,0] neg_lo:[1,0]
	s_nop 0
	v_pk_fma_f32 v[24:25], v[24:25], v[22:23], v[26:27] op_sel_hi:[0,1,1]
	v_pk_mul_f32 v[26:27], v[16:17], v[22:23] op_sel:[1,1] op_sel_hi:[0,1] neg_lo:[0,1]
	v_pk_fma_f32 v[22:23], v[16:17], v[22:23], v[26:27] op_sel_hi:[1,0,1]
	s_nop 0
	v_pk_mul_f32 v[26:27], v[44:45], v[22:23] op_sel:[1,1] op_sel_hi:[1,0] neg_lo:[1,0]
	s_nop 0
	v_pk_fma_f32 v[26:27], v[44:45], v[22:23], v[26:27] op_sel_hi:[0,1,1]
	ds_write2_b64 v62, v[24:25], v[26:27] offset0:160 offset1:176
	v_pk_mul_f32 v[24:25], v[16:17], v[22:23] op_sel:[1,1] op_sel_hi:[0,1] neg_lo:[0,1]
	v_pk_fma_f32 v[22:23], v[16:17], v[22:23], v[24:25] op_sel_hi:[1,0,1]
	s_nop 0
	v_pk_mul_f32 v[24:25], v[18:19], v[22:23] op_sel:[1,1] op_sel_hi:[1,0] neg_lo:[1,0]
	s_nop 0
	v_pk_fma_f32 v[18:19], v[18:19], v[22:23], v[24:25] op_sel_hi:[0,1,1]
	v_pk_mul_f32 v[24:25], v[16:17], v[22:23] op_sel:[1,1] op_sel_hi:[0,1] neg_lo:[0,1]
	v_pk_fma_f32 v[22:23], v[16:17], v[22:23], v[24:25] op_sel_hi:[1,0,1]
	s_nop 0
	v_pk_mul_f32 v[24:25], v[32:33], v[22:23] op_sel:[1,1] op_sel_hi:[1,0] neg_lo:[1,0]
	s_nop 0
	v_pk_fma_f32 v[24:25], v[32:33], v[22:23], v[24:25] op_sel_hi:[0,1,1]
	ds_write2_b64 v15, v[18:19], v[24:25] offset0:192 offset1:208
	v_pk_mul_f32 v[18:19], v[16:17], v[22:23] op_sel:[1,1] op_sel_hi:[0,1] neg_lo:[0,1]
	v_pk_fma_f32 v[18:19], v[16:17], v[22:23], v[18:19] op_sel_hi:[1,0,1]
	s_nop 0
	v_pk_mul_f32 v[22:23], v[20:21], v[18:19] op_sel:[1,1] op_sel_hi:[1,0] neg_lo:[1,0]
	s_nop 0
	v_pk_fma_f32 v[20:21], v[20:21], v[18:19], v[22:23] op_sel_hi:[0,1,1]
	v_pk_mul_f32 v[22:23], v[16:17], v[18:19] op_sel:[1,1] op_sel_hi:[0,1] neg_lo:[0,1]
	v_pk_fma_f32 v[16:17], v[16:17], v[18:19], v[22:23] op_sel_hi:[1,0,1]
	s_nop 0
	v_pk_mul_f32 v[18:19], v[36:37], v[16:17] op_sel:[1,1] op_sel_hi:[1,0] neg_lo:[1,0]
	s_nop 0
	v_pk_fma_f32 v[16:17], v[36:37], v[16:17], v[18:19] op_sel_hi:[0,1,1]
	ds_write2_b64 v13, v[20:21], v[16:17] offset0:224 offset1:240
	v_mov_b32_e32 v16, v182
	v_mov_b32_e32 v10, v176
	v_mov_b32_e32 v17, v175
	s_waitcnt lgkmcnt(0)
	s_barrier
	v_lshlrev_b32_e32 v190, 3, v16
	v_add_u32_e32 v190, 0x1000, v190
	global_load_dwordx2 v[202:203], v190, s[46:47] offset:-4096
	global_load_dwordx2 v[204:205], v190, s[46:47]
	v_add_u32_e32 v190, 0x2000, v190
	global_load_dwordx2 v[206:207], v190, s[46:47] offset:-4096
	global_load_dwordx2 v[208:209], v190, s[46:47]
	v_add_u32_e32 v190, 0x2000, v190
	global_load_dwordx2 v[210:211], v190, s[46:47] offset:-4096
	global_load_dwordx2 v[212:213], v190, s[46:47]
	v_add_u32_e32 v190, 0x2000, v190
	global_load_dwordx2 v[214:215], v190, s[46:47] offset:-4096
	global_load_dwordx2 v[216:217], v190, s[46:47]
	v_add_u32_e32 v190, 0x2000, v190
	global_load_dwordx2 v[218:219], v190, s[46:47] offset:-4096
	global_load_dwordx2 v[220:221], v190, s[46:47]
	v_add_u32_e32 v190, 0x2000, v190
	global_load_dwordx2 v[222:223], v190, s[46:47] offset:-4096
	global_load_dwordx2 v[224:225], v190, s[46:47]
	v_add_u32_e32 v190, 0x2000, v190
	global_load_dwordx2 v[226:227], v190, s[46:47] offset:-4096
	global_load_dwordx2 v[228:229], v190, s[46:47]
	v_add_u32_e32 v190, 0x2000, v190
	global_load_dwordx2 v[230:231], v190, s[46:47] offset:-4096
	global_load_dwordx2 v[232:233], v190, s[46:47]
	v_mov_b32_e32 v50, v165
	v_lshlrev_b32_e32 v13, 3, v17
	v_lshlrev_b32_e32 v48, 3, v10
	v_add3_u32 v10, 0, v13, v48
	v_xor_b32_e32 v13, 1, v17
	v_xor_b32_e32 v34, 8, v17
	v_xor_b32_e32 v36, 9, v17
	v_lshlrev_b32_e32 v13, 3, v13
	v_xor_b32_e32 v15, 2, v17
	v_xor_b32_e32 v24, 3, v17
	v_xor_b32_e32 v26, 4, v17
	v_xor_b32_e32 v28, 5, v17
	v_xor_b32_e32 v30, 6, v17
	v_xor_b32_e32 v32, 7, v17
	v_lshlrev_b32_e32 v34, 3, v34
	v_lshlrev_b32_e32 v36, 3, v36
	v_xor_b32_e32 v38, 10, v17
	v_xor_b32_e32 v40, 11, v17
	v_xor_b32_e32 v42, 12, v17
	v_xor_b32_e32 v44, 13, v17
	v_xor_b32_e32 v46, 14, v17
	v_xor_b32_e32 v17, 15, v17
	v_add3_u32 v13, 0, v13, v48
	v_lshlrev_b32_e32 v15, 3, v15
	v_lshlrev_b32_e32 v24, 3, v24
	v_lshlrev_b32_e32 v26, 3, v26
	v_lshlrev_b32_e32 v28, 3, v28
	v_lshlrev_b32_e32 v30, 3, v30
	v_lshlrev_b32_e32 v32, 3, v32
	v_add3_u32 v57, 0, v34, v48
	v_add3_u32 v58, 0, v36, v48
	v_lshlrev_b32_e32 v38, 3, v38
	v_lshlrev_b32_e32 v40, 3, v40
	v_lshlrev_b32_e32 v42, 3, v42
	v_lshlrev_b32_e32 v44, 3, v44
	v_lshlrev_b32_e32 v46, 3, v46
	v_lshlrev_b32_e32 v17, 3, v17
	ds_read_b64 v[18:19], v10
	ds_read_b64 v[20:21], v13
	v_add3_u32 v15, 0, v15, v48
	v_add3_u32 v52, 0, v24, v48
	v_add3_u32 v53, 0, v26, v48
	v_add3_u32 v54, 0, v28, v48
	v_add3_u32 v55, 0, v30, v48
	v_add3_u32 v56, 0, v32, v48
	ds_read_b64 v[34:35], v57
	ds_read_b64 v[36:37], v58
	v_add3_u32 v59, 0, v38, v48
	v_add3_u32 v60, 0, v40, v48
	v_add3_u32 v61, 0, v42, v48
	v_add3_u32 v62, 0, v44, v48
	v_add3_u32 v63, 0, v46, v48
	v_add3_u32 v64, 0, v17, v48
	v_mov_b32_e32 v17, v1
	ds_read_b64 v[22:23], v15
	ds_read_b64 v[24:25], v52
	ds_read_b64 v[26:27], v53
	ds_read_b64 v[28:29], v54
	ds_read_b64 v[30:31], v55
	ds_read_b64 v[32:33], v56
	ds_read_b64 v[38:39], v59
	ds_read_b64 v[40:41], v60
	ds_read_b64 v[42:43], v61
	ds_read_b64 v[44:45], v62
	ds_read_b64 v[46:47], v63
	ds_read_b64 v[48:49], v64
	s_waitcnt lgkmcnt(13)
	v_pk_add_f32 v[70:71], v[18:19], v[34:35]
	v_mov_b32_e32 v17, v164
	v_pk_add_f32 v[18:19], v[18:19], v[34:35] neg_lo:[0,1] neg_hi:[0,1]
	v_mov_b32_e32 v17, v166
	s_waitcnt lgkmcnt(12)
	v_pk_add_f32 v[34:35], v[20:21], v[36:37]
	v_pk_add_f32 v[20:21], v[20:21], v[36:37] neg_lo:[0,1] neg_hi:[0,1]
	v_mov_b32_e32 v66, v167
	v_mov_b32_e32 v17, v168
	v_mov_b32_e32 v68, v169
	s_nop 0
	v_pk_mul_f32 v[36:37], v[20:21], v[68:69] op_sel:[1,0] op_sel_hi:[0,0] neg_lo:[1,1] neg_hi:[0,1]
	v_mov_b32_e32 v17, v170
	v_pk_fma_f32 v[20:21], v[20:21], v[50:51], v[36:37] op_sel_hi:[1,0,1]
	s_waitcnt lgkmcnt(5)
	v_pk_add_f32 v[36:37], v[22:23], v[38:39]
	v_pk_add_f32 v[22:23], v[22:23], v[38:39] neg_lo:[0,1] neg_hi:[0,1]
	s_nop 0
	v_pk_mul_f32 v[38:39], v[22:23], v[66:67] op_sel:[1,0] op_sel_hi:[0,0] neg_lo:[1,1] neg_hi:[0,1]
	v_mov_b32_e32 v17, v171
	v_pk_fma_f32 v[22:23], v[22:23], v[66:67], v[38:39] op_sel_hi:[1,0,1]
	s_waitcnt lgkmcnt(4)
	v_pk_add_f32 v[38:39], v[24:25], v[40:41]
	v_pk_add_f32 v[24:25], v[24:25], v[40:41] neg_lo:[0,1] neg_hi:[0,1]
	s_nop 0
	v_pk_mul_f32 v[40:41], v[24:25], v[68:69] op_sel_hi:[1,0]
	s_nop 0
	v_pk_fma_f32 v[24:25], v[24:25], v[50:51], v[40:41] op_sel:[1,0,0] op_sel_hi:[0,0,1] neg_lo:[1,1,0] neg_hi:[0,1,0]
	s_waitcnt lgkmcnt(3)
	v_pk_add_f32 v[40:41], v[26:27], v[42:43]
	v_pk_add_f32 v[26:27], v[26:27], v[42:43] neg_lo:[0,1] neg_hi:[0,1]
	v_ashrrev_i32_e32 v17, 31, v16
	v_xor_b32_e32 v73, 0x80000000, v26
	v_mov_b32_e32 v72, v27
	s_waitcnt lgkmcnt(2)
	v_pk_add_f32 v[26:27], v[28:29], v[44:45]
	v_pk_add_f32 v[28:29], v[28:29], v[44:45] neg_lo:[0,1] neg_hi:[0,1]
	s_nop 0
	v_pk_mul_f32 v[42:43], v[28:29], v[68:69] op_sel_hi:[1,0] neg_lo:[0,1] neg_hi:[0,1]
	s_nop 0
	v_pk_fma_f32 v[28:29], v[28:29], v[50:51], v[42:43] op_sel:[1,0,0] op_sel_hi:[0,0,1] neg_lo:[1,1,0] neg_hi:[0,1,0]
	s_waitcnt lgkmcnt(1)
	v_pk_add_f32 v[42:43], v[30:31], v[46:47]
	v_pk_add_f32 v[30:31], v[30:31], v[46:47] neg_lo:[0,1] neg_hi:[0,1]
	s_nop 0
	v_pk_mul_f32 v[44:45], v[30:31], v[66:67] op_sel:[1,0] op_sel_hi:[0,0] neg_lo:[1,1] neg_hi:[0,1]
	s_nop 0
	v_pk_fma_f32 v[30:31], v[30:31], v[66:67], v[44:45] op_sel_hi:[1,0,1] neg_lo:[0,1,0] neg_hi:[0,1,0]
	s_waitcnt lgkmcnt(0)
	v_pk_add_f32 v[44:45], v[32:33], v[48:49]
	v_pk_add_f32 v[32:33], v[32:33], v[48:49] neg_lo:[0,1] neg_hi:[0,1]
	v_pk_add_f32 v[48:49], v[34:35], v[26:27]
	v_pk_add_f32 v[26:27], v[34:35], v[26:27] neg_lo:[0,1] neg_hi:[0,1]
	s_nop 0
	v_pk_mul_f32 v[34:35], v[26:27], v[66:67] op_sel:[1,0] op_sel_hi:[0,0] neg_lo:[1,1] neg_hi:[0,1]
	v_pk_fma_f32 v[26:27], v[26:27], v[66:67], v[34:35] op_sel_hi:[1,0,1]
	v_pk_add_f32 v[34:35], v[36:37], v[42:43]
	v_pk_add_f32 v[36:37], v[36:37], v[42:43] neg_lo:[0,1] neg_hi:[0,1]
	v_pk_mul_f32 v[46:47], v[32:33], v[68:69] op_sel:[1,0] op_sel_hi:[0,0] neg_lo:[1,1] neg_hi:[0,1]
	v_xor_b32_e32 v43, 0x80000000, v36
	v_mov_b32_e32 v42, v37
	v_pk_add_f32 v[36:37], v[38:39], v[44:45]
	v_pk_add_f32 v[38:39], v[38:39], v[44:45] neg_lo:[0,1] neg_hi:[0,1]
	v_pk_fma_f32 v[46:47], v[32:33], v[50:51], v[46:47] op_sel_hi:[1,0,1] neg_lo:[0,1,0] neg_hi:[0,1,0]
	v_pk_add_f32 v[32:33], v[70:71], v[40:41]
	v_pk_mul_f32 v[44:45], v[38:39], v[66:67] op_sel:[1,0] op_sel_hi:[0,0] neg_lo:[1,1] neg_hi:[0,1]
	v_pk_add_f32 v[40:41], v[70:71], v[40:41] neg_lo:[0,1] neg_hi:[0,1]
	v_pk_fma_f32 v[38:39], v[38:39], v[66:67], v[44:45] op_sel_hi:[1,0,1] neg_lo:[0,1,0] neg_hi:[0,1,0]
	v_pk_add_f32 v[44:45], v[32:33], v[34:35]
	v_pk_add_f32 v[32:33], v[32:33], v[34:35] neg_lo:[0,1] neg_hi:[0,1]
	v_pk_add_f32 v[34:35], v[48:49], v[36:37]
	v_pk_add_f32 v[36:37], v[48:49], v[36:37] neg_lo:[0,1] neg_hi:[0,1]
	v_pk_add_f32 v[50:51], v[44:45], v[34:35]
	v_xor_b32_e32 v49, 0x80000000, v36
	v_mov_b32_e32 v48, v37
	v_pk_add_f32 v[36:37], v[44:45], v[34:35] neg_lo:[0,1] neg_hi:[0,1]
	v_pk_add_f32 v[68:69], v[32:33], v[48:49]
	v_pk_add_f32 v[44:45], v[32:33], v[48:49] neg_lo:[0,1] neg_hi:[0,1]
	v_pk_add_f32 v[32:33], v[40:41], v[42:43]
	v_pk_add_f32 v[34:35], v[40:41], v[42:43] neg_lo:[0,1] neg_hi:[0,1]
	v_pk_add_f32 v[40:41], v[26:27], v[38:39]
	v_pk_add_f32 v[26:27], v[26:27], v[38:39] neg_lo:[0,1] neg_hi:[0,1]
	v_pk_add_f32 v[42:43], v[32:33], v[40:41] neg_lo:[0,1] neg_hi:[0,1]
	v_xor_b32_e32 v39, 0x80000000, v26
	v_mov_b32_e32 v38, v27
	v_pk_add_f32 v[26:27], v[32:33], v[40:41]
	v_pk_add_f32 v[40:41], v[20:21], v[28:29]
	v_pk_add_f32 v[20:21], v[20:21], v[28:29] neg_lo:[0,1] neg_hi:[0,1]
	v_pk_add_f32 v[32:33], v[34:35], v[38:39]
	v_pk_mul_f32 v[28:29], v[66:67], v[20:21] op_sel:[0,1] op_sel_hi:[0,0] neg_lo:[1,1] neg_hi:[1,0]
	v_pk_fma_f32 v[20:21], v[66:67], v[20:21], v[28:29] op_sel_hi:[0,1,1]
	v_pk_add_f32 v[28:29], v[22:23], v[30:31]
	v_pk_add_f32 v[22:23], v[22:23], v[30:31] neg_lo:[0,1] neg_hi:[0,1]
	v_pk_add_f32 v[38:39], v[34:35], v[38:39] neg_lo:[0,1] neg_hi:[0,1]
	v_xor_b32_e32 v31, 0x80000000, v22
	v_mov_b32_e32 v30, v23
	v_pk_add_f32 v[22:23], v[24:25], v[46:47]
	v_pk_add_f32 v[24:25], v[24:25], v[46:47] neg_lo:[0,1] neg_hi:[0,1]
	v_pk_add_f32 v[34:35], v[18:19], v[72:73]
	v_pk_mul_f32 v[46:47], v[66:67], v[24:25] op_sel:[0,1] op_sel_hi:[0,0] neg_lo:[1,1] neg_hi:[1,0]
	v_pk_fma_f32 v[24:25], v[66:67], v[24:25], v[46:47] op_sel_hi:[0,1,1] neg_lo:[1,0,0] neg_hi:[1,0,0]
	v_pk_add_f32 v[46:47], v[34:35], v[28:29]
	v_pk_add_f32 v[28:29], v[34:35], v[28:29] neg_lo:[0,1] neg_hi:[0,1]
	v_pk_add_f32 v[34:35], v[40:41], v[22:23]
	v_pk_add_f32 v[22:23], v[40:41], v[22:23] neg_lo:[0,1] neg_hi:[0,1]
	v_pk_add_f32 v[18:19], v[18:19], v[72:73] neg_lo:[0,1] neg_hi:[0,1]
	v_pk_add_f32 v[66:67], v[28:29], v[22:23] op_sel:[0,1] op_sel_hi:[1,0] neg_hi:[0,1]
	v_pk_add_f32 v[48:49], v[28:29], v[22:23] op_sel:[0,1] op_sel_hi:[1,0] neg_lo:[0,1]
	v_pk_add_f32 v[28:29], v[18:19], v[30:31]
	v_pk_add_f32 v[18:19], v[18:19], v[30:31] neg_lo:[0,1] neg_hi:[0,1]
	v_pk_add_f32 v[30:31], v[20:21], v[24:25]
	v_pk_add_f32 v[20:21], v[20:21], v[24:25] neg_lo:[0,1] neg_hi:[0,1]
	v_pk_add_f32 v[22:23], v[46:47], v[34:35]
	v_xor_b32_e32 v25, 0x80000000, v20
	v_mov_b32_e32 v24, v21
	v_lshl_add_u64 v[20:21], v[16:17], 3, s[46:47]
	s_waitcnt vmcnt(0)
	v_pk_add_f32 v[40:41], v[46:47], v[34:35] neg_lo:[0,1] neg_hi:[0,1]
	v_pk_add_f32 v[34:35], v[18:19], v[24:25]
	v_pk_add_f32 v[18:19], v[18:19], v[24:25] neg_lo:[0,1] neg_hi:[0,1]
	v_pk_add_f32 v[70:71], v[28:29], v[30:31]
	v_pk_add_f32 v[46:47], v[28:29], v[30:31] neg_lo:[0,1] neg_hi:[0,1]
	v_mov_b32_e32 v17, v1
	s_nop 0
	v_pk_mul_f32 v[24:25], v[50:51], v[202:203] op_sel:[1,1] op_sel_hi:[1,0] neg_lo:[1,0]
	s_nop 0
	v_pk_fma_f32 v[20:21], v[50:51], v[202:203], v[24:25] op_sel_hi:[0,1,1]
	v_add_u32_e32 v24, 0x200, v16
	v_ashrrev_i32_e32 v25, 31, v24
	v_lshl_add_u64 v[24:25], v[24:25], 3, s[46:47]
	s_nop 0
	v_pk_mul_f32 v[28:29], v[204:205], v[22:23] op_sel:[1,1] op_sel_hi:[0,1] neg_lo:[0,1]
	v_pk_fma_f32 v[22:23], v[204:205], v[22:23], v[28:29] op_sel_hi:[1,0,1]
	v_add_u32_e32 v24, 0x400, v16
	v_ashrrev_i32_e32 v25, 31, v24
	v_lshl_add_u64 v[24:25], v[24:25], 3, s[46:47]
	s_nop 0
	v_pk_mul_f32 v[28:29], v[26:27], v[206:207] op_sel:[1,1] op_sel_hi:[1,0] neg_lo:[1,0]
	s_nop 0
	v_pk_fma_f32 v[24:25], v[26:27], v[206:207], v[28:29] op_sel_hi:[0,1,1]
	v_add_u32_e32 v26, 0x600, v16
	v_ashrrev_i32_e32 v27, 31, v26
	v_lshl_add_u64 v[26:27], v[26:27], 3, s[46:47]
	s_nop 0
	v_pk_mul_f32 v[28:29], v[208:209], v[70:71] op_sel:[1,1] op_sel_hi:[0,1] neg_lo:[0,1]
	v_pk_fma_f32 v[26:27], v[208:209], v[70:71], v[28:29] op_sel_hi:[1,0,1]
	v_add_u32_e32 v28, 0x800, v16
	v_ashrrev_i32_e32 v29, 31, v28
	v_lshl_add_u64 v[28:29], v[28:29], 3, s[46:47]
	s_nop 0
	v_pk_mul_f32 v[30:31], v[68:69], v[210:211] op_sel:[1,1] op_sel_hi:[1,0] neg_lo:[1,0]
	s_nop 0
	v_pk_fma_f32 v[28:29], v[68:69], v[210:211], v[30:31] op_sel_hi:[0,1,1]
	v_add_u32_e32 v30, 0xa00, v16
	v_ashrrev_i32_e32 v31, 31, v30
	v_lshl_add_u64 v[30:31], v[30:31], 3, s[46:47]
	v_mov_b32_e32 v68, v169
	s_nop 0
	v_pk_mul_f32 v[50:51], v[212:213], v[66:67] op_sel:[1,1] op_sel_hi:[0,1] neg_lo:[0,1]
	v_pk_fma_f32 v[30:31], v[212:213], v[66:67], v[50:51] op_sel_hi:[1,0,1]
	v_add_u32_e32 v50, 0xc00, v16
	v_ashrrev_i32_e32 v51, 31, v50
	v_lshl_add_u64 v[50:51], v[50:51], 3, s[46:47]
	s_nop 0
	v_pk_mul_f32 v[66:67], v[32:33], v[214:215] op_sel:[1,1] op_sel_hi:[1,0] neg_lo:[1,0]
	s_nop 0
	v_pk_fma_f32 v[32:33], v[32:33], v[214:215], v[66:67] op_sel_hi:[0,1,1]
	v_add_u32_e32 v50, 0xe00, v16
	v_ashrrev_i32_e32 v51, 31, v50
	v_lshl_add_u64 v[50:51], v[50:51], 3, s[46:47]
	s_nop 0
	v_pk_mul_f32 v[66:67], v[216:217], v[34:35] op_sel:[1,1] op_sel_hi:[0,1] neg_lo:[0,1]
	v_pk_fma_f32 v[34:35], v[216:217], v[34:35], v[66:67] op_sel_hi:[1,0,1]
	v_add_u32_e32 v50, 0x1000, v16
	v_ashrrev_i32_e32 v51, 31, v50
	v_lshl_add_u64 v[50:51], v[50:51], 3, s[46:47]
	s_nop 0
	v_pk_mul_f32 v[66:67], v[36:37], v[218:219] op_sel:[1,1] op_sel_hi:[1,0] neg_lo:[1,0]
	s_nop 0
	v_pk_fma_f32 v[36:37], v[36:37], v[218:219], v[66:67] op_sel_hi:[0,1,1]
	v_add_u32_e32 v50, 0x1200, v16
	v_ashrrev_i32_e32 v51, 31, v50
	v_lshl_add_u64 v[50:51], v[50:51], 3, s[46:47]
	v_pk_add_f32 v[70:71], v[20:21], v[36:37]
	v_pk_add_f32 v[20:21], v[20:21], v[36:37] neg_lo:[0,1] neg_hi:[0,1]
	s_nop 0
	v_pk_mul_f32 v[66:67], v[40:41], v[220:221] op_sel:[1,1] op_sel_hi:[1,0] neg_lo:[1,0]
	s_nop 0
	v_pk_fma_f32 v[40:41], v[40:41], v[220:221], v[66:67] op_sel_hi:[0,1,1]
	v_add_u32_e32 v50, 0x1400, v16
	v_ashrrev_i32_e32 v51, 31, v50
	v_lshl_add_u64 v[50:51], v[50:51], 3, s[46:47]
	v_pk_add_f32 v[36:37], v[22:23], v[40:41]
	v_pk_add_f32 v[22:23], v[22:23], v[40:41] neg_lo:[0,1] neg_hi:[0,1]
	s_nop 0
	v_pk_mul_f32 v[66:67], v[42:43], v[222:223] op_sel:[1,1] op_sel_hi:[1,0] neg_lo:[1,0]
	s_nop 0
	v_pk_fma_f32 v[42:43], v[42:43], v[222:223], v[66:67] op_sel_hi:[0,1,1]
	v_add_u32_e32 v50, 0x1600, v16
	v_ashrrev_i32_e32 v51, 31, v50
	v_lshl_add_u64 v[50:51], v[50:51], 3, s[46:47]
	s_nop 0
	v_pk_mul_f32 v[66:67], v[46:47], v[224:225] op_sel:[1,1] op_sel_hi:[1,0] neg_lo:[1,0]
	s_nop 0
	v_pk_fma_f32 v[46:47], v[46:47], v[224:225], v[66:67] op_sel_hi:[0,1,1]
	v_add_u32_e32 v50, 0x1800, v16
	v_ashrrev_i32_e32 v51, 31, v50
	v_lshl_add_u64 v[50:51], v[50:51], 3, s[46:47]
	s_nop 0
	v_pk_mul_f32 v[66:67], v[44:45], v[226:227] op_sel:[1,1] op_sel_hi:[1,0] neg_lo:[1,0]
	s_nop 0
	v_pk_fma_f32 v[44:45], v[44:45], v[226:227], v[66:67] op_sel_hi:[0,1,1]
	v_add_u32_e32 v50, 0x1a00, v16
	v_ashrrev_i32_e32 v51, 31, v50
	v_lshl_add_u64 v[50:51], v[50:51], 3, s[46:47]
	s_nop 0
	v_pk_mul_f32 v[66:67], v[48:49], v[228:229] op_sel:[1,1] op_sel_hi:[1,0] neg_lo:[1,0]
	s_nop 0
	v_pk_fma_f32 v[48:49], v[48:49], v[228:229], v[66:67] op_sel_hi:[0,1,1]
	v_add_u32_e32 v50, 0x1c00, v16
	v_ashrrev_i32_e32 v51, 31, v50
	v_lshl_add_u64 v[50:51], v[50:51], 3, s[46:47]
	s_nop 0
	v_pk_mul_f32 v[66:67], v[38:39], v[230:231] op_sel:[1,1] op_sel_hi:[1,0] neg_lo:[1,0]
	s_nop 0
	v_pk_fma_f32 v[38:39], v[38:39], v[230:231], v[66:67] op_sel_hi:[0,1,1]
	v_add_u32_e32 v50, 0x1e00, v16
	v_ashrrev_i32_e32 v51, 31, v50
	v_lshl_add_u64 v[50:51], v[50:51], 3, s[46:47]
	v_mov_b32_e32 v50, v232
	v_mov_b32_e32 v51, v233
	v_lshlrev_b32_e32 v190, 3, v16
	v_add_u32_e32 v190, 0x11000, v190
	global_load_dwordx2 v[202:203], v190, s[46:47] offset:-4096
	global_load_dwordx2 v[204:205], v190, s[46:47]
	v_add_u32_e32 v190, 0x2000, v190
	global_load_dwordx2 v[206:207], v190, s[46:47] offset:-4096
	global_load_dwordx2 v[208:209], v190, s[46:47]
	v_add_u32_e32 v190, 0x2000, v190
	global_load_dwordx2 v[210:211], v190, s[46:47] offset:-4096
	global_load_dwordx2 v[212:213], v190, s[46:47]
	v_add_u32_e32 v190, 0x2000, v190
	global_load_dwordx2 v[214:215], v190, s[46:47] offset:-4096
	global_load_dwordx2 v[216:217], v190, s[46:47]
	v_add_u32_e32 v190, 0x2000, v190
	global_load_dwordx2 v[218:219], v190, s[46:47] offset:-4096
	global_load_dwordx2 v[220:221], v190, s[46:47]
	v_add_u32_e32 v190, 0x2000, v190
	global_load_dwordx2 v[222:223], v190, s[46:47] offset:-4096
	global_load_dwordx2 v[224:225], v190, s[46:47]
	v_add_u32_e32 v190, 0x2000, v190
	global_load_dwordx2 v[226:227], v190, s[46:47] offset:-4096
	global_load_dwordx2 v[228:229], v190, s[46:47]
	v_add_u32_e32 v190, 0x2000, v190
	global_load_dwordx2 v[230:231], v190, s[46:47] offset:-4096
	global_load_dwordx2 v[232:233], v190, s[46:47]
	v_mov_b32_e32 v17, v164
	s_nop 0
	v_pk_mul_f32 v[66:67], v[18:19], v[50:51] op_sel:[1,1] op_sel_hi:[1,0] neg_lo:[1,0]
	s_nop 0
	v_pk_fma_f32 v[18:19], v[18:19], v[50:51], v[66:67] op_sel_hi:[0,1,1]
	v_mov_b32_e32 v50, v165
	v_mov_b32_e32 v17, v166
	v_mov_b32_e32 v66, v167
	v_mov_b32_e32 v17, v168
	s_nop 0
	v_pk_mul_f32 v[40:41], v[22:23], v[68:69] op_sel:[1,0] op_sel_hi:[0,0] neg_lo:[1,0]
	v_mov_b32_e32 v17, v170
	v_pk_fma_f32 v[22:23], v[22:23], v[50:51], v[40:41] op_sel_hi:[1,0,1]
	v_pk_add_f32 v[40:41], v[24:25], v[42:43]
	v_pk_add_f32 v[24:25], v[24:25], v[42:43] neg_lo:[0,1] neg_hi:[0,1]
	s_nop 0
	v_pk_mul_f32 v[42:43], v[24:25], v[66:67] op_sel:[1,0] op_sel_hi:[0,0] neg_lo:[1,0]
	v_mov_b32_e32 v17, v171
	v_pk_fma_f32 v[24:25], v[24:25], v[66:67], v[42:43] op_sel_hi:[1,0,1]
	v_pk_add_f32 v[42:43], v[26:27], v[46:47]
	v_pk_add_f32 v[26:27], v[26:27], v[46:47] neg_lo:[0,1] neg_hi:[0,1]
	s_nop 0
	v_pk_mul_f32 v[46:47], v[26:27], v[68:69] op_sel_hi:[1,0]
	s_nop 0
	v_pk_fma_f32 v[26:27], v[26:27], v[50:51], v[46:47] op_sel:[1,0,0] op_sel_hi:[0,0,1] neg_lo:[1,0,0]
	v_pk_add_f32 v[46:47], v[28:29], v[44:45]
	v_pk_add_f32 v[28:29], v[28:29], v[44:45] neg_lo:[0,1] neg_hi:[0,1]
	v_mov_b32_e32 v17, v175
	v_xor_b32_e32 v44, 0x80000000, v29
	v_mov_b32_e32 v45, v28
	v_pk_add_f32 v[28:29], v[30:31], v[48:49]
	v_pk_add_f32 v[30:31], v[30:31], v[48:49] neg_lo:[0,1] neg_hi:[0,1]
	s_nop 0
	v_pk_mul_f32 v[48:49], v[30:31], v[68:69] op_sel_hi:[1,0] neg_lo:[0,1] neg_hi:[0,1]
	s_nop 0
	v_pk_fma_f32 v[30:31], v[30:31], v[50:51], v[48:49] op_sel:[1,0,0] op_sel_hi:[0,0,1] neg_lo:[1,0,0]
	v_pk_add_f32 v[48:49], v[32:33], v[38:39]
	v_pk_add_f32 v[32:33], v[32:33], v[38:39] neg_lo:[0,1] neg_hi:[0,1]
	s_nop 0
	v_pk_mul_f32 v[38:39], v[32:33], v[66:67] op_sel:[1,0] op_sel_hi:[0,0] neg_lo:[1,0]
	s_nop 0
	v_pk_fma_f32 v[32:33], v[32:33], v[66:67], v[38:39] op_sel_hi:[1,0,1] neg_lo:[0,1,0] neg_hi:[0,1,0]
	v_pk_add_f32 v[38:39], v[34:35], v[18:19]
	v_pk_add_f32 v[18:19], v[34:35], v[18:19] neg_lo:[0,1] neg_hi:[0,1]
	s_nop 0
	v_pk_mul_f32 v[34:35], v[18:19], v[68:69] op_sel:[1,0] op_sel_hi:[0,0] neg_lo:[1,0]
	v_mov_b32_e32 v68, v169
	v_pk_fma_f32 v[18:19], v[18:19], v[50:51], v[34:35] op_sel_hi:[1,0,1] neg_lo:[0,1,0] neg_hi:[0,1,0]
	v_pk_add_f32 v[50:51], v[36:37], v[28:29]
	v_pk_add_f32 v[28:29], v[36:37], v[28:29] neg_lo:[0,1] neg_hi:[0,1]
	v_pk_add_f32 v[34:35], v[70:71], v[46:47]
	v_pk_mul_f32 v[36:37], v[28:29], v[66:67] op_sel:[1,0] op_sel_hi:[0,0] neg_lo:[1,0]
	v_pk_add_f32 v[46:47], v[70:71], v[46:47] neg_lo:[0,1] neg_hi:[0,1]
	v_pk_fma_f32 v[28:29], v[28:29], v[66:67], v[36:37] op_sel_hi:[1,0,1]
	v_pk_add_f32 v[36:37], v[40:41], v[48:49]
	v_pk_add_f32 v[40:41], v[40:41], v[48:49] neg_lo:[0,1] neg_hi:[0,1]
	s_nop 0
	v_xor_b32_e32 v48, 0x80000000, v41
	v_mov_b32_e32 v49, v40
	v_pk_add_f32 v[40:41], v[42:43], v[38:39]
	v_pk_add_f32 v[38:39], v[42:43], v[38:39] neg_lo:[0,1] neg_hi:[0,1]
	s_nop 0
	v_pk_mul_f32 v[42:43], v[66:67], v[38:39] op_sel:[0,1] op_sel_hi:[0,0] neg_lo:[0,1]
	v_pk_fma_f32 v[38:39], v[38:39], v[66:67], v[42:43] op_sel_hi:[1,0,1] neg_lo:[0,1,0] neg_hi:[0,1,0]
	v_pk_add_f32 v[42:43], v[34:35], v[36:37]
	v_pk_add_f32 v[34:35], v[34:35], v[36:37] neg_lo:[0,1] neg_hi:[0,1]
	v_pk_add_f32 v[36:37], v[50:51], v[40:41]
	v_pk_add_f32 v[40:41], v[50:51], v[40:41] neg_lo:[0,1] neg_hi:[0,1]
	s_nop 0
	v_xor_b32_e32 v50, 0x80000000, v41
	v_mov_b32_e32 v51, v40
	v_pk_add_f32 v[40:41], v[42:43], v[36:37]
	v_pk_add_f32 v[36:37], v[42:43], v[36:37] neg_lo:[0,1] neg_hi:[0,1]
	v_pk_add_f32 v[42:43], v[34:35], v[50:51]
	v_pk_add_f32 v[34:35], v[34:35], v[50:51] neg_lo:[0,1] neg_hi:[0,1]
	v_pk_add_f32 v[50:51], v[46:47], v[48:49]
	v_pk_add_f32 v[46:47], v[46:47], v[48:49] neg_lo:[0,1] neg_hi:[0,1]
	v_pk_add_f32 v[48:49], v[28:29], v[38:39]
	v_pk_add_f32 v[28:29], v[28:29], v[38:39] neg_lo:[0,1] neg_hi:[0,1]
	s_nop 0
	v_xor_b32_e32 v38, 0x80000000, v29
	v_mov_b32_e32 v39, v28
	v_pk_add_f32 v[28:29], v[50:51], v[48:49]
	v_pk_add_f32 v[48:49], v[50:51], v[48:49] neg_lo:[0,1] neg_hi:[0,1]
	v_pk_add_f32 v[50:51], v[46:47], v[38:39]
	v_pk_add_f32 v[38:39], v[46:47], v[38:39] neg_lo:[0,1] neg_hi:[0,1]
	v_pk_add_f32 v[46:47], v[20:21], v[44:45]
	v_pk_add_f32 v[20:21], v[20:21], v[44:45] neg_lo:[0,1] neg_hi:[0,1]
	v_pk_add_f32 v[44:45], v[22:23], v[30:31]
	v_pk_add_f32 v[22:23], v[22:23], v[30:31] neg_lo:[0,1] neg_hi:[0,1]
	s_nop 0
	v_pk_mul_f32 v[30:31], v[66:67], v[22:23] op_sel:[0,1] op_sel_hi:[0,0] neg_lo:[0,1]
	v_pk_fma_f32 v[22:23], v[66:67], v[22:23], v[30:31] op_sel_hi:[0,1,1]
	v_pk_add_f32 v[30:31], v[24:25], v[32:33]
	v_pk_add_f32 v[24:25], v[24:25], v[32:33] neg_lo:[0,1] neg_hi:[0,1]
	s_nop 0
	v_xor_b32_e32 v32, 0x80000000, v25
	v_mov_b32_e32 v33, v24
	v_pk_add_f32 v[24:25], v[26:27], v[18:19]
	v_pk_add_f32 v[18:19], v[26:27], v[18:19] neg_lo:[0,1] neg_hi:[0,1]
	s_nop 0
	v_pk_mul_f32 v[26:27], v[66:67], v[18:19] op_sel:[0,1] op_sel_hi:[0,0] neg_lo:[0,1]
	v_pk_fma_f32 v[18:19], v[66:67], v[18:19], v[26:27] op_sel_hi:[0,1,1] neg_lo:[1,0,0] neg_hi:[1,0,0]
	v_pk_add_f32 v[26:27], v[46:47], v[30:31]
	v_pk_add_f32 v[30:31], v[46:47], v[30:31] neg_lo:[0,1] neg_hi:[0,1]
	v_pk_add_f32 v[46:47], v[44:45], v[24:25]
	v_pk_add_f32 v[24:25], v[44:45], v[24:25] neg_lo:[0,1] neg_hi:[0,1]
	v_mov_b32_e32 v66, v167
	v_xor_b32_e32 v44, 0x80000000, v25
	v_mov_b32_e32 v45, v24
	v_pk_add_f32 v[24:25], v[26:27], v[46:47]
	v_pk_add_f32 v[26:27], v[26:27], v[46:47] neg_lo:[0,1] neg_hi:[0,1]
	v_pk_add_f32 v[46:47], v[30:31], v[44:45]
	v_pk_add_f32 v[30:31], v[30:31], v[44:45] neg_lo:[0,1] neg_hi:[0,1]
	v_pk_add_f32 v[44:45], v[20:21], v[32:33]
	v_pk_add_f32 v[20:21], v[20:21], v[32:33] neg_lo:[0,1] neg_hi:[0,1]
	v_pk_add_f32 v[32:33], v[22:23], v[18:19]
	v_pk_add_f32 v[18:19], v[22:23], v[18:19] neg_lo:[0,1] neg_hi:[0,1]
	s_nop 0
	v_xor_b32_e32 v22, 0x80000000, v19
	v_mov_b32_e32 v23, v18
	v_pk_add_f32 v[18:19], v[44:45], v[32:33]
	v_pk_add_f32 v[32:33], v[44:45], v[32:33] neg_lo:[0,1] neg_hi:[0,1]
	v_pk_add_f32 v[44:45], v[20:21], v[22:23]
	v_pk_add_f32 v[20:21], v[20:21], v[22:23] neg_lo:[0,1] neg_hi:[0,1]
	ds_write_b64 v10, v[40:41]
	ds_write_b64 v13, v[24:25]
	ds_write_b64 v15, v[28:29]
	ds_write_b64 v52, v[18:19]
	ds_write_b64 v53, v[42:43]
	ds_write_b64 v54, v[46:47]
	ds_write_b64 v55, v[50:51]
	ds_write_b64 v56, v[44:45]
	ds_write_b64 v57, v[36:37]
	ds_write_b64 v58, v[26:27]
	ds_write_b64 v59, v[48:49]
	ds_write_b64 v60, v[32:33]
	ds_write_b64 v61, v[34:35]
	ds_write_b64 v62, v[30:31]
	ds_write_b64 v63, v[38:39]
	ds_write_b64 v64, v[20:21]
	v_mov_b32_e32 v10, v177
	v_mov_b32_e32 v64, v165
	v_lshlrev_b32_e32 v13, 3, v17
	v_lshlrev_b32_e32 v48, 3, v10
	v_add3_u32 v10, 0, v13, v48
	v_xor_b32_e32 v13, 1, v17
	v_xor_b32_e32 v34, 8, v17
	v_xor_b32_e32 v36, 9, v17
	v_lshlrev_b32_e32 v13, 3, v13
	v_xor_b32_e32 v15, 2, v17
	v_xor_b32_e32 v24, 3, v17
	v_xor_b32_e32 v26, 4, v17
	v_xor_b32_e32 v28, 5, v17
	v_xor_b32_e32 v30, 6, v17
	v_xor_b32_e32 v32, 7, v17
	v_lshlrev_b32_e32 v34, 3, v34
	v_lshlrev_b32_e32 v36, 3, v36
	v_xor_b32_e32 v38, 10, v17
	v_xor_b32_e32 v40, 11, v17
	v_xor_b32_e32 v42, 12, v17
	v_xor_b32_e32 v44, 13, v17
	v_xor_b32_e32 v46, 14, v17
	v_xor_b32_e32 v17, 15, v17
	v_add3_u32 v13, 0, v13, v48
	v_lshlrev_b32_e32 v15, 3, v15
	v_lshlrev_b32_e32 v24, 3, v24
	v_lshlrev_b32_e32 v26, 3, v26
	v_lshlrev_b32_e32 v28, 3, v28
	v_lshlrev_b32_e32 v30, 3, v30
	v_lshlrev_b32_e32 v32, 3, v32
	v_add3_u32 v55, 0, v34, v48
	v_add3_u32 v56, 0, v36, v48
	v_lshlrev_b32_e32 v38, 3, v38
	v_lshlrev_b32_e32 v40, 3, v40
	v_lshlrev_b32_e32 v42, 3, v42
	v_lshlrev_b32_e32 v44, 3, v44
	v_lshlrev_b32_e32 v46, 3, v46
	v_lshlrev_b32_e32 v17, 3, v17
	ds_read_b64 v[18:19], v10
	ds_read_b64 v[20:21], v13
	v_add3_u32 v15, 0, v15, v48
	v_add3_u32 v50, 0, v24, v48
	v_add3_u32 v51, 0, v26, v48
	v_add3_u32 v52, 0, v28, v48
	v_add3_u32 v53, 0, v30, v48
	v_add3_u32 v54, 0, v32, v48
	ds_read_b64 v[34:35], v55
	ds_read_b64 v[36:37], v56
	v_add3_u32 v57, 0, v38, v48
	v_add3_u32 v58, 0, v40, v48
	v_add3_u32 v59, 0, v42, v48
	v_add3_u32 v60, 0, v44, v48
	v_add3_u32 v61, 0, v46, v48
	v_add3_u32 v62, 0, v17, v48
	v_mov_b32_e32 v17, v1
	ds_read_b64 v[22:23], v15
	ds_read_b64 v[24:25], v50
	ds_read_b64 v[26:27], v51
	ds_read_b64 v[28:29], v52
	ds_read_b64 v[30:31], v53
	ds_read_b64 v[32:33], v54
	ds_read_b64 v[38:39], v57
	ds_read_b64 v[40:41], v58
	ds_read_b64 v[42:43], v59
	ds_read_b64 v[44:45], v60
	ds_read_b64 v[46:47], v61
	ds_read_b64 v[48:49], v62
	s_waitcnt lgkmcnt(13)
	v_pk_add_f32 v[70:71], v[18:19], v[34:35]
	v_mov_b32_e32 v17, v164
	v_pk_add_f32 v[18:19], v[18:19], v[34:35] neg_lo:[0,1] neg_hi:[0,1]
	v_mov_b32_e32 v17, v166
	s_waitcnt lgkmcnt(12)
	v_pk_add_f32 v[34:35], v[20:21], v[36:37]
	v_pk_add_f32 v[20:21], v[20:21], v[36:37] neg_lo:[0,1] neg_hi:[0,1]
	v_mov_b32_e32 v17, v168
	s_nop 0
	v_pk_mul_f32 v[36:37], v[20:21], v[68:69] op_sel:[1,0] op_sel_hi:[0,0] neg_lo:[1,1] neg_hi:[0,1]
	v_mov_b32_e32 v17, v170
	v_pk_fma_f32 v[20:21], v[20:21], v[64:65], v[36:37] op_sel_hi:[1,0,1]
	s_waitcnt lgkmcnt(5)
	v_pk_add_f32 v[36:37], v[22:23], v[38:39]
	v_pk_add_f32 v[22:23], v[22:23], v[38:39] neg_lo:[0,1] neg_hi:[0,1]
	s_nop 0
	v_pk_mul_f32 v[38:39], v[22:23], v[66:67] op_sel:[1,0] op_sel_hi:[0,0] neg_lo:[1,1] neg_hi:[0,1]
	v_mov_b32_e32 v17, v171
	v_pk_fma_f32 v[22:23], v[22:23], v[66:67], v[38:39] op_sel_hi:[1,0,1]
	s_waitcnt lgkmcnt(4)
	v_pk_add_f32 v[38:39], v[24:25], v[40:41]
	v_pk_add_f32 v[24:25], v[24:25], v[40:41] neg_lo:[0,1] neg_hi:[0,1]
	s_nop 0
	v_pk_mul_f32 v[40:41], v[24:25], v[68:69] op_sel_hi:[1,0]
	s_nop 0
	v_pk_fma_f32 v[24:25], v[24:25], v[64:65], v[40:41] op_sel:[1,0,0] op_sel_hi:[0,0,1] neg_lo:[1,1,0] neg_hi:[0,1,0]
	s_waitcnt lgkmcnt(3)
	v_pk_add_f32 v[40:41], v[26:27], v[42:43]
	v_pk_add_f32 v[26:27], v[26:27], v[42:43] neg_lo:[0,1] neg_hi:[0,1]
	s_nop 0
	v_xor_b32_e32 v73, 0x80000000, v26
	v_mov_b32_e32 v72, v27
	s_waitcnt lgkmcnt(2)
	v_pk_add_f32 v[26:27], v[28:29], v[44:45]
	v_pk_add_f32 v[28:29], v[28:29], v[44:45] neg_lo:[0,1] neg_hi:[0,1]
	s_nop 0
	v_pk_mul_f32 v[42:43], v[28:29], v[68:69] op_sel_hi:[1,0] neg_lo:[0,1] neg_hi:[0,1]
	s_nop 0
	v_pk_fma_f32 v[28:29], v[28:29], v[64:65], v[42:43] op_sel:[1,0,0] op_sel_hi:[0,0,1] neg_lo:[1,1,0] neg_hi:[0,1,0]
	s_waitcnt lgkmcnt(1)
	v_pk_add_f32 v[42:43], v[30:31], v[46:47]
	v_pk_add_f32 v[30:31], v[30:31], v[46:47] neg_lo:[0,1] neg_hi:[0,1]
	s_nop 0
	v_pk_mul_f32 v[44:45], v[30:31], v[66:67] op_sel:[1,0] op_sel_hi:[0,0] neg_lo:[1,1] neg_hi:[0,1]
	s_nop 0
	v_pk_fma_f32 v[30:31], v[30:31], v[66:67], v[44:45] op_sel_hi:[1,0,1] neg_lo:[0,1,0] neg_hi:[0,1,0]
	s_waitcnt lgkmcnt(0)
	v_pk_add_f32 v[44:45], v[32:33], v[48:49]
	v_pk_add_f32 v[32:33], v[32:33], v[48:49] neg_lo:[0,1] neg_hi:[0,1]
	v_pk_add_f32 v[48:49], v[34:35], v[26:27]
	v_pk_add_f32 v[26:27], v[34:35], v[26:27] neg_lo:[0,1] neg_hi:[0,1]
	s_nop 0
	v_pk_mul_f32 v[34:35], v[26:27], v[66:67] op_sel:[1,0] op_sel_hi:[0,0] neg_lo:[1,1] neg_hi:[0,1]
	v_pk_fma_f32 v[26:27], v[26:27], v[66:67], v[34:35] op_sel_hi:[1,0,1]
	v_pk_add_f32 v[34:35], v[36:37], v[42:43]
	v_pk_add_f32 v[36:37], v[36:37], v[42:43] neg_lo:[0,1] neg_hi:[0,1]
	v_pk_mul_f32 v[46:47], v[32:33], v[68:69] op_sel:[1,0] op_sel_hi:[0,0] neg_lo:[1,1] neg_hi:[0,1]
	v_xor_b32_e32 v43, 0x80000000, v36
	v_mov_b32_e32 v42, v37
	v_pk_add_f32 v[36:37], v[38:39], v[44:45]
	v_pk_add_f32 v[38:39], v[38:39], v[44:45] neg_lo:[0,1] neg_hi:[0,1]
	v_pk_fma_f32 v[46:47], v[32:33], v[64:65], v[46:47] op_sel_hi:[1,0,1] neg_lo:[0,1,0] neg_hi:[0,1,0]
	v_pk_add_f32 v[32:33], v[70:71], v[40:41]
	v_pk_mul_f32 v[44:45], v[38:39], v[66:67] op_sel:[1,0] op_sel_hi:[0,0] neg_lo:[1,1] neg_hi:[0,1]
	v_pk_add_f32 v[40:41], v[70:71], v[40:41] neg_lo:[0,1] neg_hi:[0,1]
	v_pk_fma_f32 v[38:39], v[38:39], v[66:67], v[44:45] op_sel_hi:[1,0,1] neg_lo:[0,1,0] neg_hi:[0,1,0]
	v_pk_add_f32 v[44:45], v[32:33], v[34:35]
	v_pk_add_f32 v[32:33], v[32:33], v[34:35] neg_lo:[0,1] neg_hi:[0,1]
	v_pk_add_f32 v[34:35], v[48:49], v[36:37]
	v_pk_add_f32 v[36:37], v[48:49], v[36:37] neg_lo:[0,1] neg_hi:[0,1]
	v_pk_add_f32 v[64:65], v[44:45], v[34:35]
	v_xor_b32_e32 v49, 0x80000000, v36
	v_mov_b32_e32 v48, v37
	v_pk_add_f32 v[36:37], v[44:45], v[34:35] neg_lo:[0,1] neg_hi:[0,1]
	v_pk_add_f32 v[68:69], v[32:33], v[48:49]
	v_pk_add_f32 v[44:45], v[32:33], v[48:49] neg_lo:[0,1] neg_hi:[0,1]
	v_pk_add_f32 v[32:33], v[40:41], v[42:43]
	v_pk_add_f32 v[34:35], v[40:41], v[42:43] neg_lo:[0,1] neg_hi:[0,1]
	v_pk_add_f32 v[40:41], v[26:27], v[38:39]
	v_pk_add_f32 v[26:27], v[26:27], v[38:39] neg_lo:[0,1] neg_hi:[0,1]
	v_pk_add_f32 v[42:43], v[32:33], v[40:41] neg_lo:[0,1] neg_hi:[0,1]
	v_xor_b32_e32 v39, 0x80000000, v26
	v_mov_b32_e32 v38, v27
	v_pk_add_f32 v[26:27], v[32:33], v[40:41]
	v_pk_add_f32 v[40:41], v[20:21], v[28:29]
	v_pk_add_f32 v[20:21], v[20:21], v[28:29] neg_lo:[0,1] neg_hi:[0,1]
	v_pk_add_f32 v[32:33], v[34:35], v[38:39]
	v_pk_mul_f32 v[28:29], v[66:67], v[20:21] op_sel:[0,1] op_sel_hi:[0,0] neg_lo:[1,1] neg_hi:[1,0]
	v_pk_fma_f32 v[20:21], v[66:67], v[20:21], v[28:29] op_sel_hi:[0,1,1]
	v_pk_add_f32 v[28:29], v[22:23], v[30:31]
	v_pk_add_f32 v[22:23], v[22:23], v[30:31] neg_lo:[0,1] neg_hi:[0,1]
	v_pk_add_f32 v[38:39], v[34:35], v[38:39] neg_lo:[0,1] neg_hi:[0,1]
	v_xor_b32_e32 v31, 0x80000000, v22
	v_mov_b32_e32 v30, v23
	v_pk_add_f32 v[22:23], v[24:25], v[46:47]
	v_pk_add_f32 v[24:25], v[24:25], v[46:47] neg_lo:[0,1] neg_hi:[0,1]
	v_pk_add_f32 v[34:35], v[18:19], v[72:73]
	v_pk_mul_f32 v[46:47], v[66:67], v[24:25] op_sel:[0,1] op_sel_hi:[0,0] neg_lo:[1,1] neg_hi:[1,0]
	v_pk_fma_f32 v[24:25], v[66:67], v[24:25], v[46:47] op_sel_hi:[0,1,1] neg_lo:[1,0,0] neg_hi:[1,0,0]
	v_pk_add_f32 v[46:47], v[34:35], v[28:29]
	v_pk_add_f32 v[28:29], v[34:35], v[28:29] neg_lo:[0,1] neg_hi:[0,1]
	v_pk_add_f32 v[34:35], v[40:41], v[22:23]
	v_pk_add_f32 v[22:23], v[40:41], v[22:23] neg_lo:[0,1] neg_hi:[0,1]
	v_pk_add_f32 v[18:19], v[18:19], v[72:73] neg_lo:[0,1] neg_hi:[0,1]
	v_pk_add_f32 v[66:67], v[28:29], v[22:23] op_sel:[0,1] op_sel_hi:[1,0] neg_hi:[0,1]
	v_pk_add_f32 v[48:49], v[28:29], v[22:23] op_sel:[0,1] op_sel_hi:[1,0] neg_lo:[0,1]
	v_pk_add_f32 v[28:29], v[18:19], v[30:31]
	v_pk_add_f32 v[18:19], v[18:19], v[30:31] neg_lo:[0,1] neg_hi:[0,1]
	v_pk_add_f32 v[30:31], v[20:21], v[24:25]
	v_pk_add_f32 v[20:21], v[20:21], v[24:25] neg_lo:[0,1] neg_hi:[0,1]
	v_pk_add_f32 v[22:23], v[46:47], v[34:35]
	v_xor_b32_e32 v25, 0x80000000, v20
	v_add_u32_e32 v20, 0x2000, v16
	v_mov_b32_e32 v24, v21
	v_ashrrev_i32_e32 v21, 31, v20
	v_lshl_add_u64 v[20:21], v[20:21], 3, s[46:47]
	s_waitcnt vmcnt(0)
	v_pk_add_f32 v[40:41], v[46:47], v[34:35] neg_lo:[0,1] neg_hi:[0,1]
	v_pk_add_f32 v[34:35], v[18:19], v[24:25]
	v_pk_add_f32 v[18:19], v[18:19], v[24:25] neg_lo:[0,1] neg_hi:[0,1]
	v_pk_add_f32 v[70:71], v[28:29], v[30:31]
	v_pk_add_f32 v[46:47], v[28:29], v[30:31] neg_lo:[0,1] neg_hi:[0,1]
	s_nop 0
	v_pk_mul_f32 v[24:25], v[64:65], v[202:203] op_sel:[1,1] op_sel_hi:[1,0] neg_lo:[1,0]
	s_nop 0
	v_pk_fma_f32 v[20:21], v[64:65], v[202:203], v[24:25] op_sel_hi:[0,1,1]
	v_add_u32_e32 v24, 0x2200, v16
	v_ashrrev_i32_e32 v25, 31, v24
	v_lshl_add_u64 v[24:25], v[24:25], 3, s[46:47]
	s_nop 0
	v_pk_mul_f32 v[28:29], v[204:205], v[22:23] op_sel:[1,1] op_sel_hi:[0,1] neg_lo:[0,1]
	v_pk_fma_f32 v[22:23], v[204:205], v[22:23], v[28:29] op_sel_hi:[1,0,1]
	v_add_u32_e32 v24, 0x2400, v16
	v_ashrrev_i32_e32 v25, 31, v24
	v_lshl_add_u64 v[24:25], v[24:25], 3, s[46:47]
	s_nop 0
	v_pk_mul_f32 v[28:29], v[26:27], v[206:207] op_sel:[1,1] op_sel_hi:[1,0] neg_lo:[1,0]
	s_nop 0
	v_pk_fma_f32 v[24:25], v[26:27], v[206:207], v[28:29] op_sel_hi:[0,1,1]
	v_add_u32_e32 v26, 0x2600, v16
	v_ashrrev_i32_e32 v27, 31, v26
	v_lshl_add_u64 v[26:27], v[26:27], 3, s[46:47]
	s_nop 0
	v_pk_mul_f32 v[28:29], v[208:209], v[70:71] op_sel:[1,1] op_sel_hi:[0,1] neg_lo:[0,1]
	v_pk_fma_f32 v[26:27], v[208:209], v[70:71], v[28:29] op_sel_hi:[1,0,1]
	v_add_u32_e32 v28, 0x2800, v16
	v_ashrrev_i32_e32 v29, 31, v28
	v_lshl_add_u64 v[28:29], v[28:29], 3, s[46:47]
	s_nop 0
	v_pk_mul_f32 v[30:31], v[68:69], v[210:211] op_sel:[1,1] op_sel_hi:[1,0] neg_lo:[1,0]
	s_nop 0
	v_pk_fma_f32 v[28:29], v[68:69], v[210:211], v[30:31] op_sel_hi:[0,1,1]
	v_add_u32_e32 v30, 0x2a00, v16
	v_ashrrev_i32_e32 v31, 31, v30
	v_lshl_add_u64 v[30:31], v[30:31], 3, s[46:47]
	s_nop 0
	v_pk_mul_f32 v[64:65], v[212:213], v[66:67] op_sel:[1,1] op_sel_hi:[0,1] neg_lo:[0,1]
	v_pk_fma_f32 v[30:31], v[212:213], v[66:67], v[64:65] op_sel_hi:[1,0,1]
	v_add_u32_e32 v64, 0x2c00, v16
	v_ashrrev_i32_e32 v65, 31, v64
	v_lshl_add_u64 v[64:65], v[64:65], 3, s[46:47]
	s_nop 0
	v_pk_mul_f32 v[66:67], v[32:33], v[214:215] op_sel:[1,1] op_sel_hi:[1,0] neg_lo:[1,0]
	s_nop 0
	v_pk_fma_f32 v[32:33], v[32:33], v[214:215], v[66:67] op_sel_hi:[0,1,1]
	v_add_u32_e32 v64, 0x2e00, v16
	v_ashrrev_i32_e32 v65, 31, v64
	v_lshl_add_u64 v[64:65], v[64:65], 3, s[46:47]
	s_nop 0
	v_pk_mul_f32 v[66:67], v[216:217], v[34:35] op_sel:[1,1] op_sel_hi:[0,1] neg_lo:[0,1]
	v_pk_fma_f32 v[34:35], v[216:217], v[34:35], v[66:67] op_sel_hi:[1,0,1]
	v_add_u32_e32 v64, 0x3000, v16
	v_ashrrev_i32_e32 v65, 31, v64
	v_lshl_add_u64 v[64:65], v[64:65], 3, s[46:47]
	s_nop 0
	v_pk_mul_f32 v[66:67], v[36:37], v[218:219] op_sel:[1,1] op_sel_hi:[1,0] neg_lo:[1,0]
	s_nop 0
	v_pk_fma_f32 v[36:37], v[36:37], v[218:219], v[66:67] op_sel_hi:[0,1,1]
	v_add_u32_e32 v64, 0x3200, v16
	v_ashrrev_i32_e32 v65, 31, v64
	v_lshl_add_u64 v[64:65], v[64:65], 3, s[46:47]
	v_pk_add_f32 v[68:69], v[20:21], v[36:37]
	v_pk_add_f32 v[20:21], v[20:21], v[36:37] neg_lo:[0,1] neg_hi:[0,1]
	s_nop 0
	v_pk_mul_f32 v[66:67], v[40:41], v[220:221] op_sel:[1,1] op_sel_hi:[1,0] neg_lo:[1,0]
	s_nop 0
	v_pk_fma_f32 v[40:41], v[40:41], v[220:221], v[66:67] op_sel_hi:[0,1,1]
	v_add_u32_e32 v64, 0x3400, v16
	v_ashrrev_i32_e32 v65, 31, v64
	v_lshl_add_u64 v[64:65], v[64:65], 3, s[46:47]
	v_pk_add_f32 v[36:37], v[22:23], v[40:41]
	v_pk_add_f32 v[22:23], v[22:23], v[40:41] neg_lo:[0,1] neg_hi:[0,1]
	s_nop 0
	v_pk_mul_f32 v[66:67], v[42:43], v[222:223] op_sel:[1,1] op_sel_hi:[1,0] neg_lo:[1,0]
	s_nop 0
	v_pk_fma_f32 v[42:43], v[42:43], v[222:223], v[66:67] op_sel_hi:[0,1,1]
	v_add_u32_e32 v64, 0x3600, v16
	v_ashrrev_i32_e32 v65, 31, v64
	v_lshl_add_u64 v[64:65], v[64:65], 3, s[46:47]
	s_nop 0
	v_pk_mul_f32 v[66:67], v[46:47], v[224:225] op_sel:[1,1] op_sel_hi:[1,0] neg_lo:[1,0]
	s_nop 0
	v_pk_fma_f32 v[46:47], v[46:47], v[224:225], v[66:67] op_sel_hi:[0,1,1]
	v_add_u32_e32 v64, 0x3800, v16
	v_ashrrev_i32_e32 v65, 31, v64
	v_lshl_add_u64 v[64:65], v[64:65], 3, s[46:47]
	s_nop 0
	v_pk_mul_f32 v[66:67], v[44:45], v[226:227] op_sel:[1,1] op_sel_hi:[1,0] neg_lo:[1,0]
	s_nop 0
	v_pk_fma_f32 v[44:45], v[44:45], v[226:227], v[66:67] op_sel_hi:[0,1,1]
	v_add_u32_e32 v64, 0x3a00, v16
	v_ashrrev_i32_e32 v65, 31, v64
	v_lshl_add_u64 v[64:65], v[64:65], 3, s[46:47]
	s_nop 0
	v_pk_mul_f32 v[66:67], v[48:49], v[228:229] op_sel:[1,1] op_sel_hi:[1,0] neg_lo:[1,0]
	s_nop 0
	v_pk_fma_f32 v[48:49], v[48:49], v[228:229], v[66:67] op_sel_hi:[0,1,1]
	v_add_u32_e32 v64, 0x3c00, v16
	v_ashrrev_i32_e32 v65, 31, v64
	v_lshl_add_u64 v[64:65], v[64:65], 3, s[46:47]
	v_add_u32_e32 v16, 0x3e00, v16
	v_ashrrev_i32_e32 v17, 31, v16
	v_lshl_add_u64 v[16:17], v[16:17], 3, s[46:47]
	s_nop 0
	v_pk_mul_f32 v[66:67], v[38:39], v[230:231] op_sel:[1,1] op_sel_hi:[1,0] neg_lo:[1,0]
	s_nop 0
	v_pk_fma_f32 v[38:39], v[38:39], v[230:231], v[66:67] op_sel_hi:[0,1,1]
	s_nop 0
	v_pk_mul_f32 v[64:65], v[18:19], v[232:233] op_sel:[1,1] op_sel_hi:[1,0] neg_lo:[1,0]
	v_mov_b32_e32 v66, v169
	v_pk_fma_f32 v[16:17], v[18:19], v[232:233], v[64:65] op_sel_hi:[0,1,1]
	v_mov_b32_e32 v18, v1
	v_mov_b32_e32 v19, v166
	v_mov_b32_e32 v18, v164
	v_mov_b32_e32 v64, v167
	v_mov_b32_e32 v18, v165
	s_nop 0
	v_mov_b32_e32 v19, v168
	s_nop 0
	v_mov_b32_e32 v19, v170
	v_pk_mul_f32 v[40:41], v[22:23], v[66:67] op_sel:[1,0] op_sel_hi:[0,0] neg_lo:[1,0]
	v_mov_b32_e32 v19, v171
	s_nop 0
	v_pk_fma_f32 v[22:23], v[22:23], v[18:19], v[40:41] op_sel_hi:[1,0,1]
	v_pk_add_f32 v[40:41], v[24:25], v[42:43]
	v_pk_add_f32 v[24:25], v[24:25], v[42:43] neg_lo:[0,1] neg_hi:[0,1]
	s_nop 0
	v_pk_mul_f32 v[42:43], v[24:25], v[64:65] op_sel:[1,0] op_sel_hi:[0,0] neg_lo:[1,0]
	s_nop 0
	v_pk_fma_f32 v[24:25], v[24:25], v[64:65], v[42:43] op_sel_hi:[1,0,1]
	v_pk_add_f32 v[42:43], v[26:27], v[46:47]
	v_pk_add_f32 v[26:27], v[26:27], v[46:47] neg_lo:[0,1] neg_hi:[0,1]
	s_nop 0
	v_pk_mul_f32 v[46:47], v[26:27], v[66:67] op_sel_hi:[1,0]
	s_nop 0
	v_pk_fma_f32 v[26:27], v[26:27], v[18:19], v[46:47] op_sel:[1,0,0] op_sel_hi:[0,0,1] neg_lo:[1,0,0]
	v_pk_add_f32 v[46:47], v[28:29], v[44:45]
	v_pk_add_f32 v[28:29], v[28:29], v[44:45] neg_lo:[0,1] neg_hi:[0,1]
	s_nop 0
	v_xor_b32_e32 v44, 0x80000000, v29
	v_mov_b32_e32 v45, v28
	v_pk_add_f32 v[28:29], v[30:31], v[48:49]
	v_pk_add_f32 v[30:31], v[30:31], v[48:49] neg_lo:[0,1] neg_hi:[0,1]
	s_nop 0
	v_pk_mul_f32 v[48:49], v[30:31], v[66:67] op_sel_hi:[1,0] neg_lo:[0,1] neg_hi:[0,1]
	s_nop 0
	v_pk_fma_f32 v[30:31], v[30:31], v[18:19], v[48:49] op_sel:[1,0,0] op_sel_hi:[0,0,1] neg_lo:[1,0,0]
	v_pk_add_f32 v[48:49], v[32:33], v[38:39]
	v_pk_add_f32 v[32:33], v[32:33], v[38:39] neg_lo:[0,1] neg_hi:[0,1]
	s_nop 0
	v_pk_mul_f32 v[38:39], v[32:33], v[64:65] op_sel:[1,0] op_sel_hi:[0,0] neg_lo:[1,0]
	s_nop 0
	v_pk_fma_f32 v[32:33], v[32:33], v[64:65], v[38:39] op_sel_hi:[1,0,1] neg_lo:[0,1,0] neg_hi:[0,1,0]
	v_pk_add_f32 v[38:39], v[34:35], v[16:17]
	v_pk_add_f32 v[16:17], v[34:35], v[16:17] neg_lo:[0,1] neg_hi:[0,1]
	s_nop 0
	v_pk_mul_f32 v[34:35], v[16:17], v[66:67] op_sel:[1,0] op_sel_hi:[0,0] neg_lo:[1,0]
	s_nop 0
	v_pk_fma_f32 v[16:17], v[16:17], v[18:19], v[34:35] op_sel_hi:[1,0,1] neg_lo:[0,1,0] neg_hi:[0,1,0]
	v_pk_add_f32 v[18:19], v[68:69], v[46:47]
	v_pk_add_f32 v[34:35], v[68:69], v[46:47] neg_lo:[0,1] neg_hi:[0,1]
	v_pk_add_f32 v[46:47], v[36:37], v[28:29]
	v_pk_add_f32 v[28:29], v[36:37], v[28:29] neg_lo:[0,1] neg_hi:[0,1]
	s_nop 0
	v_pk_mul_f32 v[36:37], v[28:29], v[64:65] op_sel:[1,0] op_sel_hi:[0,0] neg_lo:[1,0]
	s_nop 0
	v_pk_fma_f32 v[28:29], v[28:29], v[64:65], v[36:37] op_sel_hi:[1,0,1]
	v_pk_add_f32 v[36:37], v[40:41], v[48:49]
	v_pk_add_f32 v[40:41], v[40:41], v[48:49] neg_lo:[0,1] neg_hi:[0,1]
	s_nop 0
	v_xor_b32_e32 v48, 0x80000000, v41
	v_mov_b32_e32 v49, v40
	v_pk_add_f32 v[40:41], v[42:43], v[38:39]
	v_pk_add_f32 v[38:39], v[42:43], v[38:39] neg_lo:[0,1] neg_hi:[0,1]
	s_nop 0
	v_pk_mul_f32 v[42:43], v[64:65], v[38:39] op_sel:[0,1] op_sel_hi:[0,0] neg_lo:[0,1]
	v_pk_fma_f32 v[38:39], v[38:39], v[64:65], v[42:43] op_sel_hi:[1,0,1] neg_lo:[0,1,0] neg_hi:[0,1,0]
	v_pk_add_f32 v[42:43], v[18:19], v[36:37]
	v_pk_add_f32 v[18:19], v[18:19], v[36:37] neg_lo:[0,1] neg_hi:[0,1]
	v_pk_add_f32 v[36:37], v[46:47], v[40:41]
	v_pk_add_f32 v[40:41], v[46:47], v[40:41] neg_lo:[0,1] neg_hi:[0,1]
	s_nop 0
	v_xor_b32_e32 v46, 0x80000000, v41
	v_mov_b32_e32 v47, v40
	v_pk_add_f32 v[40:41], v[42:43], v[36:37]
	v_pk_add_f32 v[36:37], v[42:43], v[36:37] neg_lo:[0,1] neg_hi:[0,1]
	v_pk_add_f32 v[42:43], v[18:19], v[46:47]
	v_pk_add_f32 v[18:19], v[18:19], v[46:47] neg_lo:[0,1] neg_hi:[0,1]
	v_pk_add_f32 v[46:47], v[34:35], v[48:49]
	v_pk_add_f32 v[34:35], v[34:35], v[48:49] neg_lo:[0,1] neg_hi:[0,1]
	v_pk_add_f32 v[48:49], v[28:29], v[38:39]
	v_pk_add_f32 v[28:29], v[28:29], v[38:39] neg_lo:[0,1] neg_hi:[0,1]
	s_nop 0
	v_xor_b32_e32 v38, 0x80000000, v29
	v_mov_b32_e32 v39, v28
	v_pk_add_f32 v[28:29], v[46:47], v[48:49]
	v_pk_add_f32 v[46:47], v[46:47], v[48:49] neg_lo:[0,1] neg_hi:[0,1]
	v_pk_add_f32 v[48:49], v[34:35], v[38:39]
	v_pk_add_f32 v[34:35], v[34:35], v[38:39] neg_lo:[0,1] neg_hi:[0,1]
	v_pk_add_f32 v[38:39], v[20:21], v[44:45]
	v_pk_add_f32 v[20:21], v[20:21], v[44:45] neg_lo:[0,1] neg_hi:[0,1]
	v_pk_add_f32 v[44:45], v[22:23], v[30:31]
	v_pk_add_f32 v[22:23], v[22:23], v[30:31] neg_lo:[0,1] neg_hi:[0,1]
	s_nop 0
	v_pk_mul_f32 v[30:31], v[64:65], v[22:23] op_sel:[0,1] op_sel_hi:[0,0] neg_lo:[0,1]
	v_pk_fma_f32 v[22:23], v[64:65], v[22:23], v[30:31] op_sel_hi:[0,1,1]
	v_pk_add_f32 v[30:31], v[24:25], v[32:33]
	v_pk_add_f32 v[24:25], v[24:25], v[32:33] neg_lo:[0,1] neg_hi:[0,1]
	s_nop 0
	v_xor_b32_e32 v32, 0x80000000, v25
	v_mov_b32_e32 v33, v24
	v_pk_add_f32 v[24:25], v[26:27], v[16:17]
	v_pk_add_f32 v[16:17], v[26:27], v[16:17] neg_lo:[0,1] neg_hi:[0,1]
	s_nop 0
	v_pk_mul_f32 v[26:27], v[64:65], v[16:17] op_sel:[0,1] op_sel_hi:[0,0] neg_lo:[0,1]
	v_pk_fma_f32 v[16:17], v[64:65], v[16:17], v[26:27] op_sel_hi:[0,1,1] neg_lo:[1,0,0] neg_hi:[1,0,0]
	v_pk_add_f32 v[26:27], v[38:39], v[30:31]
	v_pk_add_f32 v[30:31], v[38:39], v[30:31] neg_lo:[0,1] neg_hi:[0,1]
	v_pk_add_f32 v[38:39], v[44:45], v[24:25]
	v_pk_add_f32 v[24:25], v[44:45], v[24:25] neg_lo:[0,1] neg_hi:[0,1]
	s_nop 0
	v_xor_b32_e32 v44, 0x80000000, v25
	v_mov_b32_e32 v45, v24
	v_pk_add_f32 v[24:25], v[26:27], v[38:39]
	v_pk_add_f32 v[26:27], v[26:27], v[38:39] neg_lo:[0,1] neg_hi:[0,1]
	v_pk_add_f32 v[38:39], v[30:31], v[44:45]
	v_pk_add_f32 v[30:31], v[30:31], v[44:45] neg_lo:[0,1] neg_hi:[0,1]
	v_pk_add_f32 v[44:45], v[20:21], v[32:33]
	v_pk_add_f32 v[20:21], v[20:21], v[32:33] neg_lo:[0,1] neg_hi:[0,1]
	v_pk_add_f32 v[32:33], v[22:23], v[16:17]
	v_pk_add_f32 v[16:17], v[22:23], v[16:17] neg_lo:[0,1] neg_hi:[0,1]
	s_nop 0
	v_xor_b32_e32 v22, 0x80000000, v17
	v_mov_b32_e32 v23, v16
	v_pk_add_f32 v[16:17], v[44:45], v[32:33]
	v_pk_add_f32 v[32:33], v[44:45], v[32:33] neg_lo:[0,1] neg_hi:[0,1]
	v_pk_add_f32 v[44:45], v[20:21], v[22:23]
	v_pk_add_f32 v[20:21], v[20:21], v[22:23] neg_lo:[0,1] neg_hi:[0,1]
	ds_write_b64 v10, v[40:41]
	ds_write_b64 v13, v[24:25]
	ds_write_b64 v15, v[28:29]
	ds_write_b64 v50, v[16:17]
	ds_write_b64 v51, v[42:43]
	ds_write_b64 v52, v[38:39]
	ds_write_b64 v53, v[48:49]
	ds_write_b64 v54, v[44:45]
	ds_write_b64 v55, v[36:37]
	ds_write_b64 v56, v[26:27]
	ds_write_b64 v57, v[46:47]
	ds_write_b64 v58, v[32:33]
	ds_write_b64 v59, v[18:19]
	ds_write_b64 v60, v[30:31]
	ds_write_b64 v61, v[34:35]
	ds_write_b64 v62, v[20:21]
	v_mov_b32_e32 v10, v174
	v_mov_b32_e32 v50, v172
	s_waitcnt lgkmcnt(0)
	s_barrier
	v_add_u32_e32 v13, v50, v10
	v_lshl_add_u32 v13, v13, 3, 0
	ds_read2_b64 v[16:19], v13 offset1:16
	v_xad_u32 v15, v50, 1, v10
	v_lshl_add_u32 v15, v15, 3, 0
	s_waitcnt lgkmcnt(0)
	v_pk_fma_f32 v[16:17], v[16:17], 0, v[16:17] op_sel:[1,0,0] op_sel_hi:[0,0,1] neg_hi:[1,0,0]
	v_pk_fma_f32 v[22:23], v[180:181], s[90:91], v[180:181] op_sel:[1,0,0] op_sel_hi:[0,1,1]
	v_pk_mul_f32 v[24:25], v[22:23], v[18:19] op_sel:[1,1] op_sel_hi:[1,0] neg_hi:[0,1]
	s_nop 0
	v_pk_fma_f32 v[18:19], v[18:19], v[22:23], v[24:25] op_sel_hi:[1,0,1]
	v_pk_mul_f32 v[24:25], v[180:181], v[22:23] op_sel:[1,1] op_sel_hi:[0,1] neg_lo:[0,1]
	v_pk_fma_f32 v[26:27], v[180:181], v[22:23], v[24:25] op_sel_hi:[1,0,1]
	ds_read2_b64 v[22:25], v15 offset0:32 offset1:48
	s_waitcnt lgkmcnt(0)
	v_pk_mul_f32 v[28:29], v[22:23], v[26:27] op_sel:[1,1] op_sel_hi:[0,1] neg_hi:[1,0]
	s_nop 0
	v_pk_fma_f32 v[22:23], v[22:23], v[26:27], v[28:29] op_sel_hi:[1,0,1]
	v_pk_mul_f32 v[28:29], v[180:181], v[26:27] op_sel:[1,1] op_sel_hi:[0,1] neg_lo:[0,1]
	v_pk_fma_f32 v[26:27], v[180:181], v[26:27], v[28:29] op_sel_hi:[1,0,1]
	s_nop 0
	v_pk_mul_f32 v[28:29], v[24:25], v[26:27] op_sel:[1,1] op_sel_hi:[0,1] neg_hi:[1,0]
	s_nop 0
	v_pk_fma_f32 v[24:25], v[24:25], v[26:27], v[28:29] op_sel_hi:[1,0,1]
	v_pk_mul_f32 v[28:29], v[180:181], v[26:27] op_sel:[1,1] op_sel_hi:[0,1] neg_lo:[0,1]
	v_pk_fma_f32 v[26:27], v[180:181], v[26:27], v[28:29] op_sel_hi:[1,0,1]
	v_xad_u32 v28, v50, 2, v10
	v_lshl_add_u32 v51, v28, 3, 0
	ds_read2_b64 v[28:31], v51 offset0:64 offset1:80
	v_pk_mul_f32 v[32:33], v[180:181], v[26:27] op_sel:[1,1] op_sel_hi:[0,1] neg_lo:[0,1]
	s_waitcnt lgkmcnt(0)
	v_pk_mul_f32 v[34:35], v[28:29], v[26:27] op_sel:[1,1] op_sel_hi:[0,1] neg_hi:[1,0]
	s_nop 0
	v_pk_fma_f32 v[28:29], v[28:29], v[26:27], v[34:35] op_sel_hi:[1,0,1]
	v_pk_fma_f32 v[34:35], v[180:181], v[26:27], v[32:33] op_sel_hi:[1,0,1]
	s_nop 0
	v_pk_mul_f32 v[26:27], v[30:31], v[34:35] op_sel:[1,1] op_sel_hi:[0,1] neg_hi:[1,0]
	v_pk_fma_f32 v[26:27], v[30:31], v[34:35], v[26:27] op_sel_hi:[1,0,1]
	v_xad_u32 v30, v50, 3, v10
	v_lshl_add_u32 v54, v30, 3, 0
	ds_read2_b64 v[30:33], v54 offset0:96 offset1:112
	v_pk_mul_f32 v[36:37], v[180:181], v[34:35] op_sel:[1,1] op_sel_hi:[0,1] neg_lo:[0,1]
	v_pk_fma_f32 v[34:35], v[180:181], v[34:35], v[36:37] op_sel_hi:[1,0,1]
	s_waitcnt lgkmcnt(0)
	v_pk_mul_f32 v[36:37], v[30:31], v[34:35] op_sel:[1,1] op_sel_hi:[0,1] neg_hi:[1,0]
	s_nop 0
	v_pk_fma_f32 v[30:31], v[30:31], v[34:35], v[36:37] op_sel_hi:[1,0,1]
	v_pk_mul_f32 v[36:37], v[180:181], v[34:35] op_sel:[1,1] op_sel_hi:[0,1] neg_lo:[0,1]
	v_pk_fma_f32 v[34:35], v[180:181], v[34:35], v[36:37] op_sel_hi:[1,0,1]
	s_nop 0
	v_pk_mul_f32 v[36:37], v[32:33], v[34:35] op_sel:[1,1] op_sel_hi:[0,1] neg_hi:[1,0]
	s_nop 0
	v_pk_fma_f32 v[32:33], v[32:33], v[34:35], v[36:37] op_sel_hi:[1,0,1]
	v_pk_mul_f32 v[36:37], v[180:181], v[34:35] op_sel:[1,1] op_sel_hi:[0,1] neg_lo:[0,1]
	v_pk_fma_f32 v[38:39], v[180:181], v[34:35], v[36:37] op_sel_hi:[1,0,1]
	v_xad_u32 v34, v50, 4, v10
	v_lshl_add_u32 v55, v34, 3, 0
	ds_read2_b64 v[34:37], v55 offset0:128 offset1:144
	v_pk_mul_f32 v[40:41], v[180:181], v[38:39] op_sel:[1,1] op_sel_hi:[0,1] neg_lo:[0,1]
	s_waitcnt lgkmcnt(0)
	v_pk_mul_f32 v[42:43], v[34:35], v[38:39] op_sel:[1,1] op_sel_hi:[0,1] neg_hi:[1,0]
	s_nop 0
	v_pk_fma_f32 v[34:35], v[34:35], v[38:39], v[42:43] op_sel_hi:[1,0,1]
	v_pk_fma_f32 v[42:43], v[180:181], v[38:39], v[40:41] op_sel_hi:[1,0,1]
	s_nop 0
	v_pk_mul_f32 v[38:39], v[36:37], v[42:43] op_sel:[1,1] op_sel_hi:[0,1] neg_hi:[1,0]
	v_pk_fma_f32 v[36:37], v[36:37], v[42:43], v[38:39] op_sel_hi:[1,0,1]
	v_xad_u32 v38, v50, 5, v10
	v_lshl_add_u32 v56, v38, 3, 0
	ds_read2_b64 v[38:41], v56 offset0:160 offset1:176
	v_pk_mul_f32 v[44:45], v[180:181], v[42:43] op_sel:[1,1] op_sel_hi:[0,1] neg_lo:[0,1]
	v_pk_fma_f32 v[42:43], v[180:181], v[42:43], v[44:45] op_sel_hi:[1,0,1]
	s_waitcnt lgkmcnt(0)
	v_pk_mul_f32 v[44:45], v[38:39], v[42:43] op_sel:[1,1] op_sel_hi:[0,1] neg_hi:[1,0]
	s_nop 0
	v_pk_fma_f32 v[38:39], v[38:39], v[42:43], v[44:45] op_sel_hi:[1,0,1]
	v_pk_mul_f32 v[44:45], v[180:181], v[42:43] op_sel:[1,1] op_sel_hi:[0,1] neg_lo:[0,1]
	v_pk_fma_f32 v[42:43], v[180:181], v[42:43], v[44:45] op_sel_hi:[1,0,1]
	s_nop 0
	v_pk_mul_f32 v[44:45], v[40:41], v[42:43] op_sel:[1,1] op_sel_hi:[0,1] neg_hi:[1,0]
	s_nop 0
	v_pk_fma_f32 v[40:41], v[40:41], v[42:43], v[44:45] op_sel_hi:[1,0,1]
	v_pk_mul_f32 v[44:45], v[180:181], v[42:43] op_sel:[1,1] op_sel_hi:[0,1] neg_lo:[0,1]
	v_pk_fma_f32 v[42:43], v[180:181], v[42:43], v[44:45] op_sel_hi:[1,0,1]
	v_xad_u32 v44, v50, 6, v10
	v_lshl_add_u32 v57, v44, 3, 0
	ds_read2_b64 v[44:47], v57 offset0:192 offset1:208
	v_pk_mul_f32 v[48:49], v[180:181], v[42:43] op_sel:[1,1] op_sel_hi:[0,1] neg_lo:[0,1]
	s_waitcnt lgkmcnt(0)
	v_pk_mul_f32 v[52:53], v[44:45], v[42:43] op_sel:[1,1] op_sel_hi:[0,1] neg_hi:[1,0]
	s_nop 0
	v_pk_fma_f32 v[44:45], v[44:45], v[42:43], v[52:53] op_sel_hi:[1,0,1]
	v_pk_fma_f32 v[52:53], v[180:181], v[42:43], v[48:49] op_sel_hi:[1,0,1]
	s_nop 0
	v_pk_mul_f32 v[42:43], v[46:47], v[52:53] op_sel:[1,1] op_sel_hi:[0,1] neg_hi:[1,0]
	v_pk_fma_f32 v[42:43], v[46:47], v[52:53], v[42:43] op_sel_hi:[1,0,1]
	v_xad_u32 v46, v50, 7, v10
	v_lshl_add_u32 v58, v46, 3, 0
	ds_read2_b64 v[46:49], v58 offset0:224 offset1:240
	v_pk_mul_f32 v[60:61], v[180:181], v[52:53] op_sel:[1,1] op_sel_hi:[0,1] neg_lo:[0,1]
	v_pk_fma_f32 v[52:53], v[180:181], v[52:53], v[60:61] op_sel_hi:[1,0,1]
	s_waitcnt lgkmcnt(0)
	v_pk_mul_f32 v[60:61], v[46:47], v[52:53] op_sel:[1,1] op_sel_hi:[0,1] neg_hi:[1,0]
	s_nop 0
	v_pk_fma_f32 v[46:47], v[46:47], v[52:53], v[60:61] op_sel_hi:[1,0,1]
	v_pk_mul_f32 v[60:61], v[180:181], v[52:53] op_sel:[1,1] op_sel_hi:[0,1] neg_lo:[0,1]
	v_pk_fma_f32 v[52:53], v[180:181], v[52:53], v[60:61] op_sel_hi:[1,0,1]
	s_nop 0
	v_pk_mul_f32 v[60:61], v[48:49], v[52:53] op_sel:[1,1] op_sel_hi:[0,1] neg_hi:[1,0]
	s_nop 0
	v_pk_fma_f32 v[48:49], v[48:49], v[52:53], v[60:61] op_sel_hi:[1,0,1]
	v_pk_mul_f32 v[60:61], v[180:181], v[52:53] op_sel:[1,1] op_sel_hi:[0,1] neg_lo:[0,1]
	v_pk_fma_f32 v[64:65], v[180:181], v[52:53], v[60:61] op_sel_hi:[1,0,1]
	v_xad_u32 v52, v50, 8, v10
	v_lshl_add_u32 v52, v52, 3, 0
	v_add_u32_e32 v59, 0x800, v52
	ds_read2_b64 v[60:63], v59 offset1:16
	v_pk_mul_f32 v[66:67], v[180:181], v[64:65] op_sel:[1,1] op_sel_hi:[0,1] neg_lo:[0,1]
	v_pk_fma_f32 v[66:67], v[180:181], v[64:65], v[66:67] op_sel_hi:[1,0,1]
	s_waitcnt lgkmcnt(0)
	v_pk_mul_f32 v[52:53], v[60:61], v[64:65] op_sel:[1,1] op_sel_hi:[0,1] neg_hi:[1,0]
	v_pk_fma_f32 v[52:53], v[60:61], v[64:65], v[52:53] op_sel_hi:[1,0,1]
	v_pk_mul_f32 v[60:61], v[62:63], v[66:67] op_sel:[1,1] op_sel_hi:[0,1] neg_hi:[1,0]
	v_pk_fma_f32 v[70:71], v[62:63], v[66:67], v[60:61] op_sel_hi:[1,0,1]
	v_xad_u32 v60, v50, 9, v10
	v_lshl_add_u32 v60, v60, 3, 0
	v_add_u32_e32 v60, 0x800, v60
	ds_read2_b64 v[62:65], v60 offset0:32 offset1:48
	v_pk_mul_f32 v[68:69], v[180:181], v[66:67] op_sel:[1,1] op_sel_hi:[0,1] neg_lo:[0,1]
	v_pk_fma_f32 v[66:67], v[180:181], v[66:67], v[68:69] op_sel_hi:[1,0,1]
	s_waitcnt lgkmcnt(0)
	v_pk_mul_f32 v[68:69], v[62:63], v[66:67] op_sel:[1,1] op_sel_hi:[0,1] neg_hi:[1,0]
	s_nop 0
	v_pk_fma_f32 v[72:73], v[62:63], v[66:67], v[68:69] op_sel_hi:[1,0,1]
	v_pk_mul_f32 v[62:63], v[180:181], v[66:67] op_sel:[1,1] op_sel_hi:[0,1] neg_lo:[0,1]
	v_pk_fma_f32 v[62:63], v[180:181], v[66:67], v[62:63] op_sel_hi:[1,0,1]
	s_nop 0
	v_pk_mul_f32 v[66:67], v[64:65], v[62:63] op_sel:[1,1] op_sel_hi:[0,1] neg_hi:[1,0]
	s_nop 0
	v_pk_fma_f32 v[74:75], v[64:65], v[62:63], v[66:67] op_sel_hi:[1,0,1]
	v_pk_mul_f32 v[64:65], v[180:181], v[62:63] op_sel:[1,1] op_sel_hi:[0,1] neg_lo:[0,1]
	v_pk_fma_f32 v[66:67], v[180:181], v[62:63], v[64:65] op_sel_hi:[1,0,1]
	v_xad_u32 v61, v50, 10, v10
	v_lshl_add_u32 v61, v61, 3, 0
	v_add_u32_e32 v61, 0x800, v61
	ds_read2_b64 v[62:65], v61 offset0:64 offset1:80
	v_pk_mul_f32 v[68:69], v[180:181], v[66:67] op_sel:[1,1] op_sel_hi:[0,1] neg_lo:[0,1]
	v_pk_fma_f32 v[68:69], v[180:181], v[66:67], v[68:69] op_sel_hi:[1,0,1]
	s_waitcnt lgkmcnt(0)
	v_pk_mul_f32 v[76:77], v[62:63], v[66:67] op_sel:[1,1] op_sel_hi:[0,1] neg_hi:[1,0]
	v_pk_fma_f32 v[76:77], v[62:63], v[66:67], v[76:77] op_sel_hi:[1,0,1]
	v_pk_mul_f32 v[62:63], v[64:65], v[68:69] op_sel:[1,1] op_sel_hi:[0,1] neg_hi:[1,0]
	v_pk_fma_f32 v[78:79], v[64:65], v[68:69], v[62:63] op_sel_hi:[1,0,1]
	v_xad_u32 v62, v50, 11, v10
	v_lshl_add_u32 v62, v62, 3, 0
	v_add_u32_e32 v62, 0x800, v62
	ds_read2_b64 v[64:67], v62 offset0:96 offset1:112
	v_pk_mul_f32 v[80:81], v[180:181], v[68:69] op_sel:[1,1] op_sel_hi:[0,1] neg_lo:[0,1]
	v_pk_fma_f32 v[68:69], v[180:181], v[68:69], v[80:81] op_sel_hi:[1,0,1]
	s_waitcnt lgkmcnt(0)
	v_pk_mul_f32 v[80:81], v[64:65], v[68:69] op_sel:[1,1] op_sel_hi:[0,1] neg_hi:[1,0]
	s_nop 0
	v_pk_fma_f32 v[80:81], v[64:65], v[68:69], v[80:81] op_sel_hi:[1,0,1]
	v_pk_mul_f32 v[64:65], v[180:181], v[68:69] op_sel:[1,1] op_sel_hi:[0,1] neg_lo:[0,1]
	v_pk_fma_f32 v[64:65], v[180:181], v[68:69], v[64:65] op_sel_hi:[1,0,1]
	s_nop 0
	v_pk_mul_f32 v[68:69], v[66:67], v[64:65] op_sel:[1,1] op_sel_hi:[0,1] neg_hi:[1,0]
	s_nop 0
	v_pk_fma_f32 v[82:83], v[66:67], v[64:65], v[68:69] op_sel_hi:[1,0,1]
	v_pk_mul_f32 v[66:67], v[180:181], v[64:65] op_sel:[1,1] op_sel_hi:[0,1] neg_lo:[0,1]
	v_pk_fma_f32 v[68:69], v[180:181], v[64:65], v[66:67] op_sel_hi:[1,0,1]
	v_xad_u32 v63, v50, 12, v10
	v_lshl_add_u32 v63, v63, 3, 0
	v_add_u32_e32 v63, 0x800, v63
	ds_read2_b64 v[64:67], v63 offset0:128 offset1:144
	v_pk_mul_f32 v[84:85], v[180:181], v[68:69] op_sel:[1,1] op_sel_hi:[0,1] neg_lo:[0,1]
	v_pk_fma_f32 v[84:85], v[180:181], v[68:69], v[84:85] op_sel_hi:[1,0,1]
	s_waitcnt lgkmcnt(0)
	v_pk_mul_f32 v[86:87], v[64:65], v[68:69] op_sel:[1,1] op_sel_hi:[0,1] neg_hi:[1,0]
	v_pk_fma_f32 v[86:87], v[64:65], v[68:69], v[86:87] op_sel_hi:[1,0,1]
	v_pk_mul_f32 v[64:65], v[66:67], v[84:85] op_sel:[1,1] op_sel_hi:[0,1] neg_hi:[1,0]
	v_pk_fma_f32 v[88:89], v[66:67], v[84:85], v[64:65] op_sel_hi:[1,0,1]
	v_xad_u32 v64, v50, 13, v10
	v_lshl_add_u32 v64, v64, 3, 0
	v_add_u32_e32 v64, 0x800, v64
	ds_read2_b64 v[66:69], v64 offset0:160 offset1:176
	v_pk_mul_f32 v[90:91], v[180:181], v[84:85] op_sel:[1,1] op_sel_hi:[0,1] neg_lo:[0,1]
	v_pk_fma_f32 v[84:85], v[180:181], v[84:85], v[90:91] op_sel_hi:[1,0,1]
	s_waitcnt lgkmcnt(0)
	v_pk_mul_f32 v[90:91], v[66:67], v[84:85] op_sel:[1,1] op_sel_hi:[0,1] neg_hi:[1,0]
	s_nop 0
	v_pk_fma_f32 v[90:91], v[66:67], v[84:85], v[90:91] op_sel_hi:[1,0,1]
	v_pk_mul_f32 v[66:67], v[180:181], v[84:85] op_sel:[1,1] op_sel_hi:[0,1] neg_lo:[0,1]
	v_pk_fma_f32 v[66:67], v[180:181], v[84:85], v[66:67] op_sel_hi:[1,0,1]
	s_nop 0
	v_pk_mul_f32 v[84:85], v[68:69], v[66:67] op_sel:[1,1] op_sel_hi:[0,1] neg_hi:[1,0]
	s_nop 0
	v_pk_fma_f32 v[84:85], v[68:69], v[66:67], v[84:85] op_sel_hi:[1,0,1]
	v_pk_mul_f32 v[68:69], v[180:181], v[66:67] op_sel:[1,1] op_sel_hi:[0,1] neg_lo:[0,1]
	v_pk_fma_f32 v[92:93], v[180:181], v[66:67], v[68:69] op_sel_hi:[1,0,1]
	v_xad_u32 v65, v50, 14, v10
	v_lshl_add_u32 v65, v65, 3, 0
	v_add_u32_e32 v65, 0x800, v65
	ds_read2_b64 v[66:69], v65 offset0:192 offset1:208
	v_pk_mul_f32 v[94:95], v[180:181], v[92:93] op_sel:[1,1] op_sel_hi:[0,1] neg_lo:[0,1]
	v_xad_u32 v10, v50, 15, v10
	s_waitcnt lgkmcnt(0)
	v_pk_mul_f32 v[96:97], v[66:67], v[92:93] op_sel:[1,1] op_sel_hi:[0,1] neg_hi:[1,0]
	v_lshl_add_u32 v10, v10, 3, 0
	v_pk_fma_f32 v[96:97], v[66:67], v[92:93], v[96:97] op_sel_hi:[1,0,1]
	v_pk_fma_f32 v[92:93], v[180:181], v[92:93], v[94:95] op_sel_hi:[1,0,1]
	s_nop 0
	v_pk_mul_f32 v[66:67], v[68:69], v[92:93] op_sel:[1,1] op_sel_hi:[0,1] neg_hi:[1,0]
	v_add_u32_e32 v101, 0x800, v10
	v_pk_fma_f32 v[94:95], v[68:69], v[92:93], v[66:67] op_sel_hi:[1,0,1]
	ds_read2_b64 v[66:69], v101 offset0:224 offset1:240
	v_pk_mul_f32 v[98:99], v[180:181], v[92:93] op_sel:[1,1] op_sel_hi:[0,1] neg_lo:[0,1]
	v_pk_fma_f32 v[92:93], v[180:181], v[92:93], v[98:99] op_sel_hi:[1,0,1]
	s_waitcnt lgkmcnt(0)
	v_pk_mul_f32 v[98:99], v[66:67], v[92:93] op_sel:[1,1] op_sel_hi:[0,1] neg_hi:[1,0]
	s_nop 0
	v_pk_fma_f32 v[66:67], v[66:67], v[92:93], v[98:99] op_sel_hi:[1,0,1]
	v_pk_mul_f32 v[98:99], v[180:181], v[92:93] op_sel:[1,1] op_sel_hi:[0,1] neg_lo:[0,1]
	v_pk_fma_f32 v[20:21], v[180:181], v[92:93], v[98:99] op_sel_hi:[1,0,1]
	s_nop 0
	v_pk_mul_f32 v[92:93], v[68:69], v[20:21] op_sel:[1,1] op_sel_hi:[0,1] neg_hi:[1,0]
	s_nop 0
	v_pk_fma_f32 v[68:69], v[68:69], v[20:21], v[92:93] op_sel_hi:[1,0,1]
	v_mov_b32_e32 v10, v1
	v_pk_add_f32 v[104:105], v[16:17], v[52:53]
	v_pk_add_f32 v[16:17], v[16:17], v[52:53] neg_lo:[0,1] neg_hi:[0,1]
	v_pk_add_f32 v[52:53], v[18:19], v[70:71]
	v_pk_add_f32 v[18:19], v[18:19], v[70:71] neg_lo:[0,1] neg_hi:[0,1]
	v_mov_b32_e32 v92, v164
	v_mov_b32_e32 v20, v165
	v_mov_b32_e32 v98, v166
	v_mov_b32_e32 v10, v167
	v_mov_b32_e32 v100, v168
	v_mov_b32_e32 v50, v169
	v_mov_b32_e32 v102, v170
	v_mov_b32_e32 v21, v171
	v_pk_mul_f32 v[70:71], v[102:103], v[18:19] op_sel:[0,1] op_sel_hi:[0,0] neg_lo:[0,1]
	v_pk_fma_f32 v[18:19], v[92:93], v[18:19], v[70:71] op_sel_hi:[0,1,1]
	v_pk_add_f32 v[70:71], v[22:23], v[72:73]
	v_pk_add_f32 v[22:23], v[22:23], v[72:73] neg_lo:[0,1] neg_hi:[0,1]
	s_nop 0
	v_pk_mul_f32 v[72:73], v[50:51], v[22:23] op_sel:[0,1] op_sel_hi:[0,0] neg_lo:[0,1]
	v_pk_fma_f32 v[22:23], v[20:21], v[22:23], v[72:73] op_sel_hi:[0,1,1]
	v_pk_add_f32 v[72:73], v[24:25], v[74:75]
	v_pk_add_f32 v[24:25], v[24:25], v[74:75] neg_lo:[0,1] neg_hi:[0,1]
	s_nop 0
	v_pk_mul_f32 v[74:75], v[100:101], v[24:25] op_sel:[0,1] op_sel_hi:[0,0] neg_lo:[0,1]
	v_pk_fma_f32 v[24:25], v[98:99], v[24:25], v[74:75] op_sel_hi:[0,1,1]
	v_pk_add_f32 v[74:75], v[28:29], v[76:77]
	v_pk_add_f32 v[28:29], v[28:29], v[76:77] neg_lo:[0,1] neg_hi:[0,1]
	s_nop 0
	v_pk_mul_f32 v[76:77], v[10:11], v[28:29] op_sel:[0,1] op_sel_hi:[0,0] neg_lo:[0,1]
	v_pk_fma_f32 v[28:29], v[10:11], v[28:29], v[76:77] op_sel_hi:[0,1,1]
	v_pk_add_f32 v[76:77], v[26:27], v[78:79]
	v_pk_add_f32 v[26:27], v[26:27], v[78:79] neg_lo:[0,1] neg_hi:[0,1]
	s_nop 0
	v_pk_mul_f32 v[78:79], v[98:99], v[26:27] op_sel:[0,1] op_sel_hi:[0,0] neg_lo:[0,1]
	v_pk_fma_f32 v[26:27], v[100:101], v[26:27], v[78:79] op_sel_hi:[0,1,1]
	v_pk_add_f32 v[78:79], v[30:31], v[80:81]
	v_pk_add_f32 v[30:31], v[30:31], v[80:81] neg_lo:[0,1] neg_hi:[0,1]
	s_nop 0
	v_pk_mul_f32 v[80:81], v[20:21], v[30:31] op_sel:[0,1] op_sel_hi:[0,0] neg_lo:[0,1]
	v_pk_fma_f32 v[30:31], v[50:51], v[30:31], v[80:81] op_sel_hi:[0,1,1]
	v_pk_add_f32 v[80:81], v[32:33], v[82:83]
	v_pk_add_f32 v[32:33], v[32:33], v[82:83] neg_lo:[0,1] neg_hi:[0,1]
	s_nop 0
	v_pk_mul_f32 v[82:83], v[92:93], v[32:33] op_sel:[0,1] op_sel_hi:[0,0] neg_lo:[0,1]
	v_pk_fma_f32 v[32:33], v[102:103], v[32:33], v[82:83] op_sel_hi:[0,1,1]
	v_pk_add_f32 v[82:83], v[34:35], v[86:87]
	v_pk_add_f32 v[34:35], v[34:35], v[86:87] neg_lo:[0,1] neg_hi:[0,1]
	s_nop 0
	v_xor_b32_e32 v86, 0x80000000, v35
	v_mov_b32_e32 v87, v34
	v_pk_add_f32 v[34:35], v[36:37], v[88:89]
	v_pk_add_f32 v[36:37], v[36:37], v[88:89] neg_lo:[0,1] neg_hi:[0,1]
	s_nop 0
	v_pk_mul_f32 v[88:89], v[92:93], v[36:37] op_sel:[0,1] op_sel_hi:[0,0] neg_lo:[0,1]
	v_pk_fma_f32 v[36:37], v[102:103], v[36:37], v[88:89] op_sel_hi:[0,1,1] neg_lo:[1,0,0] neg_hi:[1,0,0]
	v_pk_add_f32 v[88:89], v[38:39], v[90:91]
	v_pk_add_f32 v[38:39], v[38:39], v[90:91] neg_lo:[0,1] neg_hi:[0,1]
	s_nop 0
	v_pk_mul_f32 v[90:91], v[20:21], v[38:39] op_sel:[0,1] op_sel_hi:[0,0] neg_lo:[0,1]
	v_pk_fma_f32 v[38:39], v[50:51], v[38:39], v[90:91] op_sel_hi:[0,1,1] neg_lo:[1,0,0] neg_hi:[1,0,0]
	v_pk_add_f32 v[90:91], v[40:41], v[84:85]
	v_pk_add_f32 v[40:41], v[40:41], v[84:85] neg_lo:[0,1] neg_hi:[0,1]
	s_nop 0
	v_pk_mul_f32 v[84:85], v[98:99], v[40:41] op_sel:[0,1] op_sel_hi:[0,0] neg_lo:[0,1]
	v_pk_fma_f32 v[40:41], v[100:101], v[40:41], v[84:85] op_sel_hi:[0,1,1] neg_lo:[1,0,0] neg_hi:[1,0,0]
	v_pk_add_f32 v[84:85], v[44:45], v[96:97]
	v_pk_add_f32 v[44:45], v[44:45], v[96:97] neg_lo:[0,1] neg_hi:[0,1]
	s_nop 0
	v_pk_mul_f32 v[96:97], v[10:11], v[44:45] op_sel:[0,1] op_sel_hi:[0,0] neg_lo:[0,1]
	v_pk_fma_f32 v[44:45], v[10:11], v[44:45], v[96:97] op_sel_hi:[0,1,1] neg_lo:[1,0,0] neg_hi:[1,0,0]
	v_pk_add_f32 v[96:97], v[42:43], v[94:95]
	v_pk_add_f32 v[42:43], v[42:43], v[94:95] neg_lo:[0,1] neg_hi:[0,1]
	s_nop 0
	v_pk_mul_f32 v[94:95], v[100:101], v[42:43] op_sel:[0,1] op_sel_hi:[0,0] neg_lo:[0,1]
	v_pk_fma_f32 v[42:43], v[98:99], v[42:43], v[94:95] op_sel_hi:[0,1,1] neg_lo:[1,0,0] neg_hi:[1,0,0]
	v_pk_add_f32 v[94:95], v[46:47], v[66:67]
	v_pk_add_f32 v[46:47], v[46:47], v[66:67] neg_lo:[0,1] neg_hi:[0,1]
	s_nop 0
	v_pk_mul_f32 v[66:67], v[50:51], v[46:47] op_sel:[0,1] op_sel_hi:[0,0] neg_lo:[0,1]
	v_pk_fma_f32 v[46:47], v[20:21], v[46:47], v[66:67] op_sel_hi:[0,1,1] neg_lo:[1,0,0] neg_hi:[1,0,0]
	v_pk_add_f32 v[66:67], v[48:49], v[68:69]
	v_pk_add_f32 v[48:49], v[48:49], v[68:69] neg_lo:[0,1] neg_hi:[0,1]
	s_nop 0
	v_pk_mul_f32 v[68:69], v[102:103], v[48:49] op_sel:[0,1] op_sel_hi:[0,0] neg_lo:[0,1]
	v_pk_fma_f32 v[48:49], v[92:93], v[48:49], v[68:69] op_sel_hi:[0,1,1] neg_lo:[1,0,0] neg_hi:[1,0,0]
	v_pk_add_f32 v[92:93], v[52:53], v[34:35]
	v_pk_add_f32 v[34:35], v[52:53], v[34:35] neg_lo:[0,1] neg_hi:[0,1]
	v_pk_add_f32 v[68:69], v[104:105], v[82:83]
	v_pk_mul_f32 v[52:53], v[50:51], v[34:35] op_sel:[0,1] op_sel_hi:[0,0] neg_lo:[0,1]
	v_pk_fma_f32 v[34:35], v[20:21], v[34:35], v[52:53] op_sel_hi:[0,1,1]
	v_pk_add_f32 v[52:53], v[70:71], v[88:89]
	v_pk_add_f32 v[70:71], v[70:71], v[88:89] neg_lo:[0,1] neg_hi:[0,1]
	v_pk_add_f32 v[82:83], v[104:105], v[82:83] neg_lo:[0,1] neg_hi:[0,1]
	v_pk_mul_f32 v[88:89], v[10:11], v[70:71] op_sel:[0,1] op_sel_hi:[0,0] neg_lo:[0,1]
	v_pk_fma_f32 v[70:71], v[10:11], v[70:71], v[88:89] op_sel_hi:[0,1,1]
	v_pk_add_f32 v[88:89], v[72:73], v[90:91]
	v_pk_add_f32 v[72:73], v[72:73], v[90:91] neg_lo:[0,1] neg_hi:[0,1]
	s_nop 0
	v_pk_mul_f32 v[90:91], v[20:21], v[72:73] op_sel:[0,1] op_sel_hi:[0,0] neg_lo:[0,1]
	v_pk_fma_f32 v[72:73], v[50:51], v[72:73], v[90:91] op_sel_hi:[0,1,1]
	v_pk_add_f32 v[90:91], v[74:75], v[84:85]
	v_pk_add_f32 v[74:75], v[74:75], v[84:85] neg_lo:[0,1] neg_hi:[0,1]
	s_nop 0
	v_xor_b32_e32 v84, 0x80000000, v75
	v_mov_b32_e32 v85, v74
	v_pk_add_f32 v[74:75], v[76:77], v[96:97]
	v_pk_add_f32 v[76:77], v[76:77], v[96:97] neg_lo:[0,1] neg_hi:[0,1]
	s_nop 0
	v_pk_mul_f32 v[96:97], v[20:21], v[76:77] op_sel:[0,1] op_sel_hi:[0,0] neg_lo:[0,1]
	v_pk_fma_f32 v[76:77], v[50:51], v[76:77], v[96:97] op_sel_hi:[0,1,1] neg_lo:[1,0,0] neg_hi:[1,0,0]
	v_pk_add_f32 v[96:97], v[78:79], v[94:95]
	v_pk_add_f32 v[78:79], v[78:79], v[94:95] neg_lo:[0,1] neg_hi:[0,1]
	s_nop 0
	v_pk_mul_f32 v[94:95], v[10:11], v[78:79] op_sel:[0,1] op_sel_hi:[0,0] neg_lo:[0,1]
	v_pk_fma_f32 v[78:79], v[10:11], v[78:79], v[94:95] op_sel_hi:[0,1,1] neg_lo:[1,0,0] neg_hi:[1,0,0]
	v_pk_add_f32 v[94:95], v[80:81], v[66:67]
	v_pk_add_f32 v[66:67], v[80:81], v[66:67] neg_lo:[0,1] neg_hi:[0,1]
	s_nop 0
	v_pk_mul_f32 v[80:81], v[50:51], v[66:67] op_sel:[0,1] op_sel_hi:[0,0] neg_lo:[0,1]
	v_pk_fma_f32 v[66:67], v[20:21], v[66:67], v[80:81] op_sel_hi:[0,1,1] neg_lo:[1,0,0] neg_hi:[1,0,0]
	v_pk_add_f32 v[80:81], v[68:69], v[90:91]
	v_pk_add_f32 v[68:69], v[68:69], v[90:91] neg_lo:[0,1] neg_hi:[0,1]
	v_pk_add_f32 v[90:91], v[92:93], v[74:75]
	v_pk_add_f32 v[74:75], v[92:93], v[74:75] neg_lo:[0,1] neg_hi:[0,1]
	s_nop 0
	v_pk_mul_f32 v[92:93], v[10:11], v[74:75] op_sel:[0,1] op_sel_hi:[0,0] neg_lo:[0,1]
	v_pk_fma_f32 v[74:75], v[10:11], v[74:75], v[92:93] op_sel_hi:[0,1,1]
	v_pk_add_f32 v[92:93], v[52:53], v[96:97]
	v_pk_add_f32 v[52:53], v[52:53], v[96:97] neg_lo:[0,1] neg_hi:[0,1]
	s_nop 0
	v_xor_b32_e32 v96, 0x80000000, v53
	v_mov_b32_e32 v97, v52
	v_pk_add_f32 v[52:53], v[88:89], v[94:95]
	v_pk_add_f32 v[88:89], v[88:89], v[94:95] neg_lo:[0,1] neg_hi:[0,1]
	s_nop 0
	v_pk_mul_f32 v[94:95], v[10:11], v[88:89] op_sel:[0,1] op_sel_hi:[0,0] neg_lo:[0,1]
	v_pk_fma_f32 v[88:89], v[10:11], v[88:89], v[94:95] op_sel_hi:[0,1,1] neg_lo:[1,0,0] neg_hi:[1,0,0]
	v_pk_add_f32 v[94:95], v[80:81], v[92:93]
	v_pk_add_f32 v[80:81], v[80:81], v[92:93] neg_lo:[0,1] neg_hi:[0,1]
	v_pk_add_f32 v[92:93], v[90:91], v[52:53]
	v_pk_add_f32 v[52:53], v[90:91], v[52:53] neg_lo:[0,1] neg_hi:[0,1]
	s_nop 0
	v_xor_b32_e32 v90, 0x80000000, v53
	v_mov_b32_e32 v91, v52
	v_pk_add_f32 v[52:53], v[94:95], v[92:93]
	v_pk_add_f32 v[92:93], v[94:95], v[92:93] neg_lo:[0,1] neg_hi:[0,1]
	v_pk_add_f32 v[94:95], v[80:81], v[90:91]
	v_pk_add_f32 v[80:81], v[80:81], v[90:91] neg_lo:[0,1] neg_hi:[0,1]
	v_pk_add_f32 v[90:91], v[68:69], v[96:97]
	v_pk_add_f32 v[68:69], v[68:69], v[96:97] neg_lo:[0,1] neg_hi:[0,1]
	v_pk_add_f32 v[96:97], v[74:75], v[88:89]
	v_pk_add_f32 v[74:75], v[74:75], v[88:89] neg_lo:[0,1] neg_hi:[0,1]
	s_nop 0
	v_xor_b32_e32 v88, 0x80000000, v75
	v_mov_b32_e32 v89, v74
	v_pk_add_f32 v[74:75], v[90:91], v[96:97]
	v_pk_add_f32 v[90:91], v[90:91], v[96:97] neg_lo:[0,1] neg_hi:[0,1]
	v_pk_add_f32 v[96:97], v[68:69], v[88:89]
	v_pk_add_f32 v[68:69], v[68:69], v[88:89] neg_lo:[0,1] neg_hi:[0,1]
	v_pk_add_f32 v[88:89], v[82:83], v[84:85]
	v_pk_add_f32 v[82:83], v[82:83], v[84:85] neg_lo:[0,1] neg_hi:[0,1]
	v_pk_add_f32 v[84:85], v[34:35], v[76:77]
	v_pk_add_f32 v[34:35], v[34:35], v[76:77] neg_lo:[0,1] neg_hi:[0,1]
	s_nop 0
	v_pk_mul_f32 v[76:77], v[10:11], v[34:35] op_sel:[0,1] op_sel_hi:[0,0] neg_lo:[0,1]
	v_pk_fma_f32 v[34:35], v[10:11], v[34:35], v[76:77] op_sel_hi:[0,1,1]
	v_pk_add_f32 v[76:77], v[70:71], v[78:79]
	v_pk_add_f32 v[70:71], v[70:71], v[78:79] neg_lo:[0,1] neg_hi:[0,1]
	s_nop 0
	v_xor_b32_e32 v78, 0x80000000, v71
	v_mov_b32_e32 v79, v70
	v_pk_add_f32 v[70:71], v[72:73], v[66:67]
	v_pk_add_f32 v[66:67], v[72:73], v[66:67] neg_lo:[0,1] neg_hi:[0,1]
	s_nop 0
	v_pk_mul_f32 v[72:73], v[10:11], v[66:67] op_sel:[0,1] op_sel_hi:[0,0] neg_lo:[0,1]
	v_pk_fma_f32 v[66:67], v[10:11], v[66:67], v[72:73] op_sel_hi:[0,1,1] neg_lo:[1,0,0] neg_hi:[1,0,0]
	v_pk_add_f32 v[72:73], v[88:89], v[76:77]
	v_pk_add_f32 v[76:77], v[88:89], v[76:77] neg_lo:[0,1] neg_hi:[0,1]
	v_pk_add_f32 v[88:89], v[84:85], v[70:71]
	v_pk_add_f32 v[70:71], v[84:85], v[70:71] neg_lo:[0,1] neg_hi:[0,1]
	s_nop 0
	v_xor_b32_e32 v84, 0x80000000, v71
	v_mov_b32_e32 v85, v70
	v_pk_add_f32 v[70:71], v[72:73], v[88:89]
	v_pk_add_f32 v[72:73], v[72:73], v[88:89] neg_lo:[0,1] neg_hi:[0,1]
	v_pk_add_f32 v[88:89], v[76:77], v[84:85]
	v_pk_add_f32 v[76:77], v[76:77], v[84:85] neg_lo:[0,1] neg_hi:[0,1]
	v_pk_add_f32 v[84:85], v[82:83], v[78:79]
	v_pk_add_f32 v[78:79], v[82:83], v[78:79] neg_lo:[0,1] neg_hi:[0,1]
	v_pk_add_f32 v[82:83], v[34:35], v[66:67]
	v_pk_add_f32 v[34:35], v[34:35], v[66:67] neg_lo:[0,1] neg_hi:[0,1]
	s_nop 0
	v_xor_b32_e32 v66, 0x80000000, v35
	v_mov_b32_e32 v67, v34
	v_pk_add_f32 v[34:35], v[84:85], v[82:83]
	v_pk_add_f32 v[82:83], v[84:85], v[82:83] neg_lo:[0,1] neg_hi:[0,1]
	v_pk_add_f32 v[84:85], v[78:79], v[66:67]
	v_pk_add_f32 v[66:67], v[78:79], v[66:67] neg_lo:[0,1] neg_hi:[0,1]
	v_pk_add_f32 v[78:79], v[16:17], v[86:87]
	v_pk_add_f32 v[16:17], v[16:17], v[86:87] neg_lo:[0,1] neg_hi:[0,1]
	v_pk_add_f32 v[86:87], v[18:19], v[36:37]
	v_pk_add_f32 v[18:19], v[18:19], v[36:37] neg_lo:[0,1] neg_hi:[0,1]
	s_nop 0
	v_pk_mul_f32 v[36:37], v[50:51], v[18:19] op_sel:[0,1] op_sel_hi:[0,0] neg_lo:[0,1]
	v_pk_fma_f32 v[18:19], v[20:21], v[18:19], v[36:37] op_sel_hi:[0,1,1]
	v_pk_add_f32 v[36:37], v[22:23], v[38:39]
	v_pk_add_f32 v[22:23], v[22:23], v[38:39] neg_lo:[0,1] neg_hi:[0,1]
	s_nop 0
	v_pk_mul_f32 v[38:39], v[10:11], v[22:23] op_sel:[0,1] op_sel_hi:[0,0] neg_lo:[0,1]
	v_pk_fma_f32 v[22:23], v[10:11], v[22:23], v[38:39] op_sel_hi:[0,1,1]
	v_pk_add_f32 v[38:39], v[24:25], v[40:41]
	v_pk_add_f32 v[24:25], v[24:25], v[40:41] neg_lo:[0,1] neg_hi:[0,1]
	s_nop 0
	v_pk_mul_f32 v[40:41], v[20:21], v[24:25] op_sel:[0,1] op_sel_hi:[0,0] neg_lo:[0,1]
	v_pk_fma_f32 v[24:25], v[50:51], v[24:25], v[40:41] op_sel_hi:[0,1,1]
	v_pk_add_f32 v[40:41], v[28:29], v[44:45]
	v_pk_add_f32 v[28:29], v[28:29], v[44:45] neg_lo:[0,1] neg_hi:[0,1]
	s_nop 0
	v_xor_b32_e32 v44, 0x80000000, v29
	v_mov_b32_e32 v45, v28
	v_pk_add_f32 v[28:29], v[26:27], v[42:43]
	v_pk_add_f32 v[26:27], v[26:27], v[42:43] neg_lo:[0,1] neg_hi:[0,1]
	s_nop 0
	v_pk_mul_f32 v[42:43], v[20:21], v[26:27] op_sel:[0,1] op_sel_hi:[0,0] neg_lo:[0,1]
	v_pk_fma_f32 v[26:27], v[50:51], v[26:27], v[42:43] op_sel_hi:[0,1,1] neg_lo:[1,0,0] neg_hi:[1,0,0]
	v_pk_add_f32 v[42:43], v[30:31], v[46:47]
	v_pk_add_f32 v[30:31], v[30:31], v[46:47] neg_lo:[0,1] neg_hi:[0,1]
	s_nop 0
	v_pk_mul_f32 v[46:47], v[10:11], v[30:31] op_sel:[0,1] op_sel_hi:[0,0] neg_lo:[0,1]
	v_pk_fma_f32 v[30:31], v[10:11], v[30:31], v[46:47] op_sel_hi:[0,1,1] neg_lo:[1,0,0] neg_hi:[1,0,0]
	v_pk_add_f32 v[46:47], v[32:33], v[48:49]
	v_pk_add_f32 v[32:33], v[32:33], v[48:49] neg_lo:[0,1] neg_hi:[0,1]
	s_nop 0
	v_pk_mul_f32 v[48:49], v[50:51], v[32:33] op_sel:[0,1] op_sel_hi:[0,0] neg_lo:[0,1]
	v_pk_fma_f32 v[20:21], v[20:21], v[32:33], v[48:49] op_sel_hi:[0,1,1] neg_lo:[1,0,0] neg_hi:[1,0,0]
	v_pk_add_f32 v[48:49], v[86:87], v[28:29]
	v_pk_add_f32 v[28:29], v[86:87], v[28:29] neg_lo:[0,1] neg_hi:[0,1]
	v_pk_add_f32 v[32:33], v[78:79], v[40:41]
	v_pk_add_f32 v[40:41], v[78:79], v[40:41] neg_lo:[0,1] neg_hi:[0,1]
	v_pk_mul_f32 v[78:79], v[10:11], v[28:29] op_sel:[0,1] op_sel_hi:[0,0] neg_lo:[0,1]
	v_pk_fma_f32 v[28:29], v[10:11], v[28:29], v[78:79] op_sel_hi:[0,1,1]
	v_pk_add_f32 v[78:79], v[36:37], v[42:43]
	v_pk_add_f32 v[36:37], v[36:37], v[42:43] neg_lo:[0,1] neg_hi:[0,1]
	s_nop 0
	v_xor_b32_e32 v42, 0x80000000, v37
	v_mov_b32_e32 v43, v36
	v_pk_add_f32 v[36:37], v[38:39], v[46:47]
	v_pk_add_f32 v[38:39], v[38:39], v[46:47] neg_lo:[0,1] neg_hi:[0,1]
	s_nop 0
	v_pk_mul_f32 v[46:47], v[10:11], v[38:39] op_sel:[0,1] op_sel_hi:[0,0] neg_lo:[0,1]
	v_pk_fma_f32 v[38:39], v[10:11], v[38:39], v[46:47] op_sel_hi:[0,1,1] neg_lo:[1,0,0] neg_hi:[1,0,0]
	v_pk_add_f32 v[46:47], v[32:33], v[78:79]
	v_pk_add_f32 v[32:33], v[32:33], v[78:79] neg_lo:[0,1] neg_hi:[0,1]
	v_pk_add_f32 v[78:79], v[48:49], v[36:37]
	v_pk_add_f32 v[36:37], v[48:49], v[36:37] neg_lo:[0,1] neg_hi:[0,1]
	s_nop 0
	v_pk_add_f32 v[86:87], v[32:33], v[36:37] op_sel:[0,1] op_sel_hi:[1,0] neg_lo:[0,1]
	v_pk_add_f32 v[32:33], v[32:33], v[36:37] op_sel:[0,1] op_sel_hi:[1,0] neg_hi:[0,1]
	v_pk_add_f32 v[48:49], v[40:41], v[42:43]
	v_pk_add_f32 v[40:41], v[40:41], v[42:43] neg_lo:[0,1] neg_hi:[0,1]
	v_pk_add_f32 v[42:43], v[28:29], v[38:39]
	v_pk_add_f32 v[28:29], v[28:29], v[38:39] neg_lo:[0,1] neg_hi:[0,1]
	v_pk_add_f32 v[36:37], v[46:47], v[78:79] neg_lo:[0,1] neg_hi:[0,1]
	v_xor_b32_e32 v38, 0x80000000, v29
	v_mov_b32_e32 v39, v28
	v_pk_add_f32 v[28:29], v[48:49], v[42:43]
	v_pk_add_f32 v[42:43], v[48:49], v[42:43] neg_lo:[0,1] neg_hi:[0,1]
	v_pk_add_f32 v[48:49], v[40:41], v[38:39]
	v_pk_add_f32 v[38:39], v[40:41], v[38:39] neg_lo:[0,1] neg_hi:[0,1]
	v_pk_add_f32 v[40:41], v[16:17], v[44:45]
	v_pk_add_f32 v[16:17], v[16:17], v[44:45] neg_lo:[0,1] neg_hi:[0,1]
	v_pk_add_f32 v[44:45], v[18:19], v[26:27]
	v_pk_add_f32 v[18:19], v[18:19], v[26:27] neg_lo:[0,1] neg_hi:[0,1]
	s_nop 0
	v_pk_mul_f32 v[26:27], v[10:11], v[18:19] op_sel:[0,1] op_sel_hi:[0,0] neg_lo:[0,1]
	v_pk_fma_f32 v[18:19], v[10:11], v[18:19], v[26:27] op_sel_hi:[0,1,1]
	v_pk_add_f32 v[26:27], v[22:23], v[30:31]
	v_pk_add_f32 v[22:23], v[22:23], v[30:31] neg_lo:[0,1] neg_hi:[0,1]
	s_nop 0
	v_xor_b32_e32 v30, 0x80000000, v23
	v_mov_b32_e32 v31, v22
	v_pk_add_f32 v[22:23], v[24:25], v[20:21]
	v_pk_add_f32 v[20:21], v[24:25], v[20:21] neg_lo:[0,1] neg_hi:[0,1]
	s_nop 0
	v_pk_mul_f32 v[24:25], v[10:11], v[20:21] op_sel:[0,1] op_sel_hi:[0,0] neg_lo:[0,1]
	v_pk_fma_f32 v[20:21], v[10:11], v[20:21], v[24:25] op_sel_hi:[0,1,1] neg_lo:[1,0,0] neg_hi:[1,0,0]
	v_pk_add_f32 v[24:25], v[40:41], v[26:27]
	v_pk_add_f32 v[26:27], v[40:41], v[26:27] neg_lo:[0,1] neg_hi:[0,1]
	v_pk_add_f32 v[40:41], v[44:45], v[22:23]
	v_pk_add_f32 v[22:23], v[44:45], v[22:23] neg_lo:[0,1] neg_hi:[0,1]
	s_nop 0
	v_xor_b32_e32 v44, 0x80000000, v23
	v_mov_b32_e32 v45, v22
	v_pk_add_f32 v[22:23], v[24:25], v[40:41]
	v_pk_add_f32 v[24:25], v[24:25], v[40:41] neg_lo:[0,1] neg_hi:[0,1]
	v_pk_add_f32 v[40:41], v[26:27], v[44:45]
	v_pk_add_f32 v[26:27], v[26:27], v[44:45] neg_lo:[0,1] neg_hi:[0,1]
	v_pk_add_f32 v[44:45], v[16:17], v[30:31]
	v_pk_add_f32 v[16:17], v[16:17], v[30:31] neg_lo:[0,1] neg_hi:[0,1]
	v_pk_add_f32 v[30:31], v[18:19], v[20:21]
	v_pk_add_f32 v[18:19], v[18:19], v[20:21] neg_lo:[0,1] neg_hi:[0,1]
	s_nop 0
	v_xor_b32_e32 v20, 0x80000000, v19
	v_mov_b32_e32 v21, v18
	v_pk_add_f32 v[18:19], v[44:45], v[30:31]
	v_pk_add_f32 v[30:31], v[44:45], v[30:31] neg_lo:[0,1] neg_hi:[0,1]
	v_pk_add_f32 v[44:45], v[16:17], v[20:21]
	v_pk_add_f32 v[16:17], v[16:17], v[20:21] neg_lo:[0,1] neg_hi:[0,1]
	v_pk_add_f32 v[20:21], v[46:47], v[78:79]
	ds_write2_b64 v13, v[52:53], v[20:21] offset1:16
	ds_write2_b64 v15, v[70:71], v[22:23] offset0:32 offset1:48
	ds_write2_b64 v51, v[74:75], v[28:29] offset0:64 offset1:80
	ds_write2_b64 v54, v[34:35], v[18:19] offset0:96 offset1:112
	ds_write2_b64 v55, v[94:95], v[86:87] offset0:128 offset1:144
	ds_write2_b64 v56, v[88:89], v[40:41] offset0:160 offset1:176
	ds_write2_b64 v57, v[96:97], v[48:49] offset0:192 offset1:208
	ds_write2_b64 v58, v[84:85], v[44:45] offset0:224 offset1:240
	ds_write2_b64 v59, v[92:93], v[36:37] offset1:16
	ds_write2_b64 v60, v[72:73], v[24:25] offset0:32 offset1:48
	ds_write2_b64 v61, v[90:91], v[42:43] offset0:64 offset1:80
	ds_write2_b64 v62, v[82:83], v[30:31] offset0:96 offset1:112
	ds_write2_b64 v63, v[80:81], v[32:33] offset0:128 offset1:144
	ds_write2_b64 v64, v[76:77], v[26:27] offset0:160 offset1:176
	ds_write2_b64 v65, v[68:69], v[38:39] offset0:192 offset1:208
	ds_write2_b64 v101, v[66:67], v[16:17] offset0:224 offset1:240
	v_mov_b32_e32 v10, v173
	s_waitcnt lgkmcnt(0)
	s_barrier
	v_lshl_add_u32 v10, v10, 3, 0
	ds_read_b64 v[16:17], v10
	ds_read_b64 v[80:81], v10 offset:4224
	ds_read_b64 v[78:79], v10 offset:8448
	ds_read_b64 v[76:77], v10 offset:12672
	ds_read_b64 v[74:75], v10 offset:16896
	ds_read_b64 v[72:73], v10 offset:21120
	ds_read_b64 v[70:71], v10 offset:25344
	ds_read_b64 v[68:69], v10 offset:29568
	ds_read_b64 v[24:25], v10 offset:33792
	ds_read_b64 v[62:63], v10 offset:38016
	ds_read_b64 v[60:61], v10 offset:42240
	ds_read_b64 v[58:59], v10 offset:46464
	ds_read_b64 v[54:55], v10 offset:50688
	ds_read_b64 v[50:51], v10 offset:54912
	ds_read_b64 v[46:47], v10 offset:59136
	ds_read_b64 v[44:45], v10 offset:63360
	v_add_u32_e32 v13, 0x10800, v10
	v_add_u32_e32 v15, 0x11880, v10
	v_add_u32_e32 v20, 0x12900, v10
	v_add_u32_e32 v21, 0x13980, v10
	ds_read_b64 v[18:19], v13
	ds_read_b64 v[66:67], v15
	ds_read_b64 v[64:65], v20
	ds_read_b64 v[38:39], v21
	v_add_u32_e32 v13, 0x14a00, v10
	v_add_u32_e32 v15, 0x15a80, v10
	v_add_u32_e32 v20, 0x16b00, v10
	v_add_u32_e32 v21, 0x17b80, v10
	ds_read_b64 v[30:31], v13
	ds_read_b64 v[56:57], v15
	ds_read_b64 v[52:53], v20
	ds_read_b64 v[48:49], v21
	v_add_u32_e32 v13, 0x18c00, v10
	v_add_u32_e32 v15, 0x19c80, v10
	v_add_u32_e32 v20, 0x1ad00, v10
	v_add_u32_e32 v21, 0x1bd80, v10
	ds_read_b64 v[82:83], v13
	ds_read_b64 v[42:43], v15
	ds_read_b64 v[40:41], v20
	ds_read_b64 v[36:37], v21
	v_add_u32_e32 v13, 0x1ce00, v10
	v_add_u32_e32 v15, 0x1de80, v10
	v_add_u32_e32 v20, 0x1ef00, v10
	v_add_u32_e32 v10, 0x1ff80, v10
	ds_read_b64 v[34:35], v13
	ds_read_b64 v[32:33], v15
	ds_read_b64 v[28:29], v20
	ds_read_b64 v[26:27], v10
	v_pk_fma_f32 v[84:85], v[178:179], s[90:91], v[178:179] op_sel:[1,0,0] op_sel_hi:[0,1,1]
	v_pk_mul_f32 v[20:21], v[178:179], v[84:85] op_sel:[1,1] op_sel_hi:[0,1] neg_lo:[0,1]
	v_pk_fma_f32 v[86:87], v[178:179], v[84:85], v[20:21] op_sel_hi:[1,0,1]
	v_mov_b32_e32 v10, v1
	v_pk_mul_f32 v[20:21], v[178:179], v[86:87] op_sel:[1,1] op_sel_hi:[0,1] neg_lo:[0,1]
	v_pk_fma_f32 v[88:89], v[178:179], v[86:87], v[20:21] op_sel_hi:[1,0,1]
	v_mov_b32_e32 v13, v171
	v_pk_mul_f32 v[20:21], v[178:179], v[88:89] op_sel:[1,1] op_sel_hi:[0,1] neg_lo:[0,1]
	v_pk_fma_f32 v[90:91], v[178:179], v[88:89], v[20:21] op_sel_hi:[1,0,1]
	v_mov_b32_e32 v10, v164
	v_pk_mul_f32 v[20:21], v[178:179], v[90:91] op_sel:[1,1] op_sel_hi:[0,1] neg_lo:[0,1]
	v_pk_fma_f32 v[92:93], v[178:179], v[90:91], v[20:21] op_sel_hi:[1,0,1]
	s_waitcnt lgkmcnt(14)
	v_fmac_f32_e32 v16, 0, v17
	v_pk_mul_f32 v[20:21], v[178:179], v[92:93] op_sel:[1,1] op_sel_hi:[0,1] neg_lo:[0,1]
	v_pk_fma_f32 v[94:95], v[178:179], v[92:93], v[20:21] op_sel_hi:[1,0,1]
	v_readlane_b32 s70, v251, 22
	v_pk_mul_f32 v[20:21], v[178:179], v[94:95] op_sel:[1,1] op_sel_hi:[0,1] neg_lo:[0,1]
	v_pk_fma_f32 v[96:97], v[178:179], v[94:95], v[20:21] op_sel_hi:[1,0,1]
	v_readlane_b32 s71, v251, 23
	v_pk_mul_f32 v[20:21], v[178:179], v[96:97] op_sel:[1,1] op_sel_hi:[0,1] neg_lo:[0,1]
	v_pk_fma_f32 v[98:99], v[178:179], v[96:97], v[20:21] op_sel_hi:[1,0,1]
	s_movk_i32 s10, 0x1000
	v_pk_mul_f32 v[20:21], v[178:179], v[98:99] op_sel:[1,1] op_sel_hi:[0,1] neg_lo:[0,1]
	v_pk_fma_f32 v[100:101], v[178:179], v[98:99], v[20:21] op_sel_hi:[1,0,1]
	s_movk_i32 s11, 0x2000
	v_pk_mul_f32 v[20:21], v[178:179], v[100:101] op_sel:[1,1] op_sel_hi:[0,1] neg_lo:[0,1]
	v_pk_fma_f32 v[102:103], v[178:179], v[100:101], v[20:21] op_sel_hi:[1,0,1]
	s_movk_i32 s13, 0x5000
	v_pk_mul_f32 v[20:21], v[178:179], v[102:103] op_sel:[1,1] op_sel_hi:[0,1] neg_lo:[0,1]
	v_pk_fma_f32 v[104:105], v[178:179], v[102:103], v[20:21] op_sel_hi:[1,0,1]
	s_movk_i32 s12, 0x6000
	v_pk_mul_f32 v[20:21], v[178:179], v[104:105] op_sel:[1,1] op_sel_hi:[0,1] neg_lo:[0,1]
	v_pk_fma_f32 v[106:107], v[178:179], v[104:105], v[20:21] op_sel_hi:[1,0,1]
	s_movk_i32 s16, 0x7000
	v_pk_mul_f32 v[20:21], v[178:179], v[106:107] op_sel:[1,1] op_sel_hi:[0,1] neg_lo:[0,1]
	v_pk_fma_f32 v[108:109], v[178:179], v[106:107], v[20:21] op_sel_hi:[1,0,1]
	s_mov_b32 s80, 0x3f74fa0b
	v_pk_mul_f32 v[20:21], v[178:179], v[108:109] op_sel:[1,1] op_sel_hi:[0,1] neg_lo:[0,1]
	v_pk_fma_f32 v[110:111], v[178:179], v[108:109], v[20:21] op_sel_hi:[1,0,1]
	s_mov_b32 s81, 0xbe94a031
	v_pk_mul_f32 v[20:21], v[178:179], v[110:111] op_sel:[1,1] op_sel_hi:[0,1] neg_lo:[0,1]
	v_pk_fma_f32 v[112:113], v[178:179], v[110:111], v[20:21] op_sel_hi:[1,0,1]
	s_mov_b32 s20, 0x3f61c598
	v_pk_mul_f32 v[20:21], v[178:179], v[112:113] op_sel:[1,1] op_sel_hi:[0,1] neg_lo:[0,1]
	v_pk_fma_f32 v[20:21], v[178:179], v[112:113], v[20:21] op_sel_hi:[1,0,1]
	s_mov_b32 s21, 0xbef15aea
	v_pk_mul_f32 v[114:115], v[178:179], v[20:21] op_sel:[1,1] op_sel_hi:[0,1] neg_lo:[0,1]
	v_pk_fma_f32 v[114:115], v[178:179], v[20:21], v[114:115] op_sel_hi:[1,0,1]
	v_mul_f32_e32 v18, v18, v20
	v_pk_mul_f32 v[116:117], v[178:179], v[114:115] op_sel:[1,1] op_sel_hi:[0,1] neg_lo:[0,1]
	v_pk_fma_f32 v[116:117], v[178:179], v[114:115], v[116:117] op_sel_hi:[1,0,1]
	v_fmac_f32_e32 v18, v19, v21
	v_pk_mul_f32 v[118:119], v[178:179], v[116:117] op_sel:[1,1] op_sel_hi:[0,1] neg_lo:[0,1]
	v_pk_fma_f32 v[118:119], v[178:179], v[116:117], v[118:119] op_sel_hi:[1,0,1]
	v_add_f32_e32 v17, v16, v18
	v_pk_mul_f32 v[120:121], v[178:179], v[118:119] op_sel:[1,1] op_sel_hi:[0,1] neg_lo:[0,1]
	v_pk_fma_f32 v[120:121], v[178:179], v[118:119], v[120:121] op_sel_hi:[1,0,1]
	s_mov_b32 s40, s45
	v_pk_mul_f32 v[122:123], v[178:179], v[120:121] op_sel:[1,1] op_sel_hi:[0,1] neg_lo:[0,1]
	v_pk_fma_f32 v[122:123], v[178:179], v[120:121], v[122:123] op_sel_hi:[1,0,1]
	s_mov_b32 s41, s94
	v_pk_mul_f32 v[124:125], v[178:179], v[122:123] op_sel:[1,1] op_sel_hi:[0,1] neg_lo:[0,1]
	v_pk_fma_f32 v[124:125], v[178:179], v[122:123], v[124:125] op_sel_hi:[1,0,1]
	s_mov_b32 s86, 0x3f226799
	v_pk_mul_f32 v[126:127], v[178:179], v[124:125] op_sel:[1,1] op_sel_hi:[0,1] neg_lo:[0,1]
	v_pk_fma_f32 v[126:127], v[178:179], v[124:125], v[126:127] op_sel_hi:[1,0,1]
	s_mov_b32 s87, 0xbf45e403
	v_pk_mul_f32 v[128:129], v[178:179], v[126:127] op_sel:[1,1] op_sel_hi:[0,1] neg_lo:[0,1]
	v_pk_fma_f32 v[128:129], v[178:179], v[126:127], v[128:129] op_sel_hi:[1,0,1]
	s_mov_b32 s24, 0x3f0e39da
	v_pk_mul_f32 v[130:131], v[178:179], v[128:129] op_sel:[1,1] op_sel_hi:[0,1] neg_lo:[0,1]
	v_pk_fma_f32 v[130:131], v[178:179], v[128:129], v[130:131] op_sel_hi:[1,0,1]
	s_mov_b32 s25, 0xbf54db31
	v_pk_mul_f32 v[132:133], v[178:179], v[130:131] op_sel:[1,1] op_sel_hi:[0,1] neg_lo:[0,1]
	v_pk_fma_f32 v[132:133], v[178:179], v[130:131], v[132:133] op_sel_hi:[1,0,1]
	s_mov_b32 s88, 0x3ef15aea
	v_pk_mul_f32 v[134:135], v[178:179], v[132:133] op_sel:[1,1] op_sel_hi:[0,1] neg_lo:[0,1]
	v_pk_fma_f32 v[134:135], v[178:179], v[132:133], v[134:135] op_sel_hi:[1,0,1]
	s_mov_b32 s89, 0xbf61c598
	v_pk_mul_f32 v[136:137], v[178:179], v[134:135] op_sel:[1,1] op_sel_hi:[0,1] neg_lo:[0,1]
	v_pk_fma_f32 v[136:137], v[178:179], v[134:135], v[136:137] op_sel_hi:[1,0,1]
	s_mov_b32 s18, 0x3ec3ef15
	v_pk_mul_f32 v[138:139], v[178:179], v[136:137] op_sel:[1,1] op_sel_hi:[0,1] neg_lo:[0,1]
	v_pk_fma_f32 v[138:139], v[178:179], v[136:137], v[138:139] op_sel_hi:[1,0,1]
	s_mov_b32 s19, 0xbf6c835e
	v_pk_mul_f32 v[140:141], v[178:179], v[138:139] op_sel:[1,1] op_sel_hi:[0,1] neg_lo:[0,1]
	v_pk_fma_f32 v[140:141], v[178:179], v[138:139], v[140:141] op_sel_hi:[1,0,1]
	s_mov_b32 s92, 0x3e94a031
	v_pk_mul_f32 v[142:143], v[178:179], v[140:141] op_sel:[1,1] op_sel_hi:[0,1] neg_lo:[0,1]
	v_pk_fma_f32 v[22:23], v[178:179], v[140:141], v[142:143] op_sel_hi:[1,0,1]
	s_waitcnt lgkmcnt(0)
	v_pk_mul_f32 v[142:143], v[26:27], v[22:23] op_sel:[1,1] op_sel_hi:[0,1] neg_hi:[1,0]
	s_mov_b32 s93, 0xbf74fa0b
	v_pk_fma_f32 v[26:27], v[26:27], v[22:23], v[142:143] op_sel_hi:[1,0,1]
	v_pk_mul_f32 v[22:23], v[28:29], v[140:141] op_sel:[1,1] op_sel_hi:[0,1] neg_hi:[1,0]
	s_mov_b32 s82, 0x3f54db31
	v_pk_fma_f32 v[28:29], v[28:29], v[140:141], v[22:23] op_sel_hi:[1,0,1]
	v_pk_mul_f32 v[22:23], v[32:33], v[138:139] op_sel:[1,1] op_sel_hi:[0,1] neg_hi:[1,0]
	s_mov_b32 s83, 0xbf0e39da
	v_pk_fma_f32 v[32:33], v[32:33], v[138:139], v[22:23] op_sel_hi:[1,0,1]
	v_pk_mul_f32 v[22:23], v[34:35], v[136:137] op_sel:[1,1] op_sel_hi:[0,1] neg_hi:[1,0]
	s_mov_b32 s28, 0x3f45e403
	v_pk_fma_f32 v[34:35], v[34:35], v[136:137], v[22:23] op_sel_hi:[1,0,1]
	v_pk_mul_f32 v[22:23], v[36:37], v[134:135] op_sel:[1,1] op_sel_hi:[0,1] neg_hi:[1,0]
	s_mov_b32 s29, 0xbf226799
	v_pk_fma_f32 v[36:37], v[36:37], v[134:135], v[22:23] op_sel_hi:[1,0,1]
	v_pk_mul_f32 v[22:23], v[40:41], v[132:133] op_sel:[1,1] op_sel_hi:[0,1] neg_hi:[1,0]
	s_mov_b32 s36, s97
	v_pk_fma_f32 v[40:41], v[40:41], v[132:133], v[22:23] op_sel_hi:[1,0,1]
	v_pk_mul_f32 v[22:23], v[42:43], v[130:131] op_sel:[1,1] op_sel_hi:[0,1] neg_hi:[1,0]
	s_mov_b32 s37, s95
	v_pk_fma_f32 v[42:43], v[42:43], v[130:131], v[22:23] op_sel_hi:[1,0,1]
	v_pk_mul_f32 v[22:23], v[82:83], v[128:129] op_sel:[1,1] op_sel_hi:[0,1] neg_hi:[1,0]
	s_mov_b32 s96, s95
	v_pk_fma_f32 v[22:23], v[82:83], v[128:129], v[22:23] op_sel_hi:[1,0,1]
	v_pk_mul_f32 v[82:83], v[48:49], v[126:127] op_sel:[1,1] op_sel_hi:[0,1] neg_hi:[1,0]
	s_mov_b32 s23, s25
	v_pk_fma_f32 v[48:49], v[48:49], v[126:127], v[82:83] op_sel_hi:[1,0,1]
	v_pk_mul_f32 v[82:83], v[52:53], v[124:125] op_sel:[1,1] op_sel_hi:[0,1] neg_hi:[1,0]
	s_mov_b32 s22, s83
	v_pk_fma_f32 v[52:53], v[52:53], v[124:125], v[82:83] op_sel_hi:[1,0,1]
	v_pk_mul_f32 v[82:83], v[56:57], v[122:123] op_sel:[1,1] op_sel_hi:[0,1] neg_hi:[1,0]
	s_mov_b32 s26, s29
	v_pk_fma_f32 v[56:57], v[56:57], v[122:123], v[82:83] op_sel_hi:[1,0,1]
	v_pk_mul_f32 v[82:83], v[30:31], v[120:121] op_sel:[1,1] op_sel_hi:[0,1] neg_hi:[1,0]
	s_mov_b32 s27, s87
	v_pk_fma_f32 v[30:31], v[30:31], v[120:121], v[82:83] op_sel_hi:[1,0,1]
	v_pk_mul_f32 v[82:83], v[38:39], v[118:119] op_sel:[1,1] op_sel_hi:[0,1] neg_hi:[1,0]
	s_movk_i32 s39, 0x2000
	v_pk_fma_f32 v[38:39], v[38:39], v[118:119], v[82:83] op_sel_hi:[1,0,1]
	v_pk_mul_f32 v[82:83], v[64:65], v[116:117] op_sel:[1,1] op_sel_hi:[0,1] neg_hi:[1,0]
	s_mov_b32 s44, s94
	v_pk_fma_f32 v[64:65], v[64:65], v[116:117], v[82:83] op_sel_hi:[1,0,1]
	v_pk_mul_f32 v[82:83], v[66:67], v[114:115] op_sel:[1,1] op_sel_hi:[0,1] neg_hi:[1,0]
	v_mov_b32_e32 v118, v164
	v_pk_fma_f32 v[66:67], v[66:67], v[114:115], v[82:83] op_sel_hi:[1,0,1]
	v_pk_mul_f32 v[82:83], v[44:45], v[112:113] op_sel:[1,1] op_sel_hi:[0,1] neg_hi:[1,0]
	v_mov_b32_e32 v120, v166
	v_pk_fma_f32 v[44:45], v[44:45], v[112:113], v[82:83] op_sel_hi:[1,0,1]
	v_pk_mul_f32 v[82:83], v[46:47], v[110:111] op_sel:[1,1] op_sel_hi:[0,1] neg_hi:[1,0]
	v_mov_b32_e32 v122, v168
	v_pk_fma_f32 v[46:47], v[46:47], v[110:111], v[82:83] op_sel_hi:[1,0,1]
	v_pk_mul_f32 v[82:83], v[50:51], v[108:109] op_sel:[1,1] op_sel_hi:[0,1] neg_hi:[1,0]
	v_mov_b32_e32 v124, v170
	v_pk_fma_f32 v[50:51], v[50:51], v[108:109], v[82:83] op_sel_hi:[1,0,1]
	v_pk_mul_f32 v[82:83], v[54:55], v[106:107] op_sel:[1,1] op_sel_hi:[0,1] neg_hi:[1,0]
	s_movk_i32 s33, 0x5000
	v_pk_fma_f32 v[54:55], v[54:55], v[106:107], v[82:83] op_sel_hi:[1,0,1]
	v_pk_mul_f32 v[82:83], v[58:59], v[104:105] op_sel:[1,1] op_sel_hi:[0,1] neg_hi:[1,0]
	s_nop 0
	v_pk_fma_f32 v[58:59], v[58:59], v[104:105], v[82:83] op_sel_hi:[1,0,1]
	v_pk_mul_f32 v[82:83], v[60:61], v[102:103] op_sel:[1,1] op_sel_hi:[0,1] neg_hi:[1,0]
	s_nop 0
	v_pk_fma_f32 v[60:61], v[60:61], v[102:103], v[82:83] op_sel_hi:[1,0,1]
	v_pk_mul_f32 v[82:83], v[62:63], v[100:101] op_sel:[1,1] op_sel_hi:[0,1] neg_hi:[1,0]
	s_nop 0
	v_pk_fma_f32 v[62:63], v[62:63], v[100:101], v[82:83] op_sel_hi:[1,0,1]
	v_pk_mul_f32 v[82:83], v[24:25], v[98:99] op_sel:[1,1] op_sel_hi:[0,1] neg_hi:[1,0]
	s_nop 0
	v_pk_fma_f32 v[24:25], v[24:25], v[98:99], v[82:83] op_sel_hi:[1,0,1]
	v_pk_mul_f32 v[82:83], v[68:69], v[96:97] op_sel:[1,1] op_sel_hi:[0,1] neg_hi:[1,0]
	v_add_f32_e32 v22, v24, v22
	v_pk_fma_f32 v[68:69], v[68:69], v[96:97], v[82:83] op_sel_hi:[1,0,1]
	v_pk_mul_f32 v[82:83], v[70:71], v[94:95] op_sel:[1,1] op_sel_hi:[0,1] neg_hi:[1,0]
	v_add_f32_e32 v20, v17, v22
	v_pk_fma_f32 v[70:71], v[70:71], v[94:95], v[82:83] op_sel_hi:[1,0,1]
	v_pk_mul_f32 v[82:83], v[72:73], v[92:93] op_sel:[1,1] op_sel_hi:[0,1] neg_hi:[1,0]
	v_mov_b32_e32 v94, v170
	v_pk_fma_f32 v[72:73], v[72:73], v[92:93], v[82:83] op_sel_hi:[1,0,1]
	v_pk_mul_f32 v[82:83], v[74:75], v[90:91] op_sel:[1,1] op_sel_hi:[0,1] neg_hi:[1,0]
	v_mov_b32_e32 v92, v169
	v_pk_fma_f32 v[74:75], v[74:75], v[90:91], v[82:83] op_sel_hi:[1,0,1]
	v_pk_mul_f32 v[82:83], v[76:77], v[88:89] op_sel:[1,1] op_sel_hi:[0,1] neg_hi:[1,0]
	v_mov_b32_e32 v90, v168
	v_pk_fma_f32 v[76:77], v[76:77], v[88:89], v[82:83] op_sel_hi:[1,0,1]
	v_pk_mul_f32 v[82:83], v[78:79], v[86:87] op_sel:[1,1] op_sel_hi:[0,1] neg_hi:[1,0]
	v_mov_b32_e32 v88, v167
	v_pk_fma_f32 v[78:79], v[78:79], v[86:87], v[82:83] op_sel_hi:[1,0,1]
	v_pk_mul_f32 v[82:83], v[84:85], v[80:81] op_sel:[1,1] op_sel_hi:[1,0] neg_hi:[0,1]
	v_mov_b32_e32 v86, v166
	v_pk_fma_f32 v[80:81], v[80:81], v[84:85], v[82:83] op_sel_hi:[1,0,1]
	v_mov_b32_e32 v84, v165
	v_pk_add_f32 v[96:97], v[80:81], v[66:67]
	v_pk_add_f32 v[66:67], v[80:81], v[66:67] neg_lo:[0,1] neg_hi:[0,1]
	s_nop 0
	v_sub_f32_e32 v82, v25, v23
	v_pk_mul_f32 v[80:81], v[94:95], v[66:67] op_sel:[0,1] op_sel_hi:[0,0] neg_lo:[0,1]
	v_pk_fma_f32 v[80:81], v[10:11], v[66:67], v[80:81] op_sel_hi:[0,1,1]
	v_pk_add_f32 v[66:67], v[78:79], v[64:65]
	v_pk_add_f32 v[64:65], v[78:79], v[64:65] neg_lo:[0,1] neg_hi:[0,1]
	s_nop 0
	v_pk_mul_f32 v[78:79], v[92:93], v[64:65] op_sel:[0,1] op_sel_hi:[0,0] neg_lo:[0,1]
	v_pk_fma_f32 v[64:65], v[84:85], v[64:65], v[78:79] op_sel_hi:[0,1,1]
	v_pk_add_f32 v[78:79], v[76:77], v[38:39]
	v_pk_add_f32 v[38:39], v[76:77], v[38:39] neg_lo:[0,1] neg_hi:[0,1]
	s_barrier
	v_pk_mul_f32 v[76:77], v[90:91], v[38:39] op_sel:[0,1] op_sel_hi:[0,0] neg_lo:[0,1]
	v_pk_fma_f32 v[76:77], v[86:87], v[38:39], v[76:77] op_sel_hi:[0,1,1]
	v_pk_add_f32 v[38:39], v[74:75], v[30:31]
	v_pk_add_f32 v[30:31], v[74:75], v[30:31] neg_lo:[0,1] neg_hi:[0,1]
	s_nop 0
	v_pk_mul_f32 v[74:75], v[88:89], v[30:31] op_sel:[0,1] op_sel_hi:[0,0] neg_lo:[0,1]
	v_pk_fma_f32 v[30:31], v[88:89], v[30:31], v[74:75] op_sel_hi:[0,1,1]
	v_pk_add_f32 v[74:75], v[72:73], v[56:57]
	v_pk_add_f32 v[56:57], v[72:73], v[56:57] neg_lo:[0,1] neg_hi:[0,1]
	v_sub_f32_e32 v22, v17, v22
	v_pk_mul_f32 v[72:73], v[86:87], v[56:57] op_sel:[0,1] op_sel_hi:[0,0] neg_lo:[0,1]
	v_pk_fma_f32 v[72:73], v[90:91], v[56:57], v[72:73] op_sel_hi:[0,1,1]
	v_pk_add_f32 v[56:57], v[70:71], v[52:53]
	v_pk_add_f32 v[52:53], v[70:71], v[52:53] neg_lo:[0,1] neg_hi:[0,1]
	v_ashrrev_i32_e32 v15, 31, v14
	v_pk_mul_f32 v[70:71], v[84:85], v[52:53] op_sel:[0,1] op_sel_hi:[0,0] neg_lo:[0,1]
	v_pk_fma_f32 v[52:53], v[92:93], v[52:53], v[70:71] op_sel_hi:[0,1,1]
	v_pk_add_f32 v[70:71], v[68:69], v[48:49]
	v_pk_add_f32 v[48:49], v[68:69], v[48:49] neg_lo:[0,1] neg_hi:[0,1]
	v_lshl_add_u64 v[14:15], v[14:15], 2, s[70:71]
	v_pk_mul_f32 v[68:69], v[10:11], v[48:49] op_sel:[0,1] op_sel_hi:[0,0] neg_lo:[0,1]
	v_pk_fma_f32 v[98:99], v[94:95], v[48:49], v[68:69] op_sel_hi:[0,1,1]
	v_pk_add_f32 v[48:49], v[62:63], v[42:43]
	v_pk_add_f32 v[42:43], v[62:63], v[42:43] neg_lo:[0,1] neg_hi:[0,1]
	s_nop 0
	v_pk_mul_f32 v[62:63], v[10:11], v[42:43] op_sel:[0,1] op_sel_hi:[0,0] neg_lo:[0,1]
	v_pk_fma_f32 v[62:63], v[94:95], v[42:43], v[62:63] op_sel_hi:[0,1,1] neg_lo:[1,0,0] neg_hi:[1,0,0]
	v_pk_add_f32 v[42:43], v[60:61], v[40:41]
	v_pk_add_f32 v[40:41], v[60:61], v[40:41] neg_lo:[0,1] neg_hi:[0,1]
	s_nop 0
	v_pk_mul_f32 v[60:61], v[84:85], v[40:41] op_sel:[0,1] op_sel_hi:[0,0] neg_lo:[0,1]
	v_pk_fma_f32 v[100:101], v[92:93], v[40:41], v[60:61] op_sel_hi:[0,1,1] neg_lo:[1,0,0] neg_hi:[1,0,0]
	v_pk_add_f32 v[60:61], v[58:59], v[36:37]
	v_pk_add_f32 v[36:37], v[58:59], v[36:37] neg_lo:[0,1] neg_hi:[0,1]
	s_nop 0
	v_pk_mul_f32 v[40:41], v[86:87], v[36:37] op_sel:[0,1] op_sel_hi:[0,0] neg_lo:[0,1]
	v_pk_fma_f32 v[58:59], v[90:91], v[36:37], v[40:41] op_sel_hi:[0,1,1] neg_lo:[1,0,0] neg_hi:[1,0,0]
	v_pk_add_f32 v[40:41], v[54:55], v[34:35]
	v_pk_add_f32 v[34:35], v[54:55], v[34:35] neg_lo:[0,1] neg_hi:[0,1]
	v_pk_add_f32 v[54:55], v[46:47], v[28:29]
	v_pk_mul_f32 v[36:37], v[88:89], v[34:35] op_sel:[0,1] op_sel_hi:[0,0] neg_lo:[0,1]
	v_pk_fma_f32 v[34:35], v[88:89], v[34:35], v[36:37] op_sel_hi:[0,1,1] neg_lo:[1,0,0] neg_hi:[1,0,0]
	v_pk_add_f32 v[36:37], v[50:51], v[32:33]
	v_pk_add_f32 v[32:33], v[50:51], v[32:33] neg_lo:[0,1] neg_hi:[0,1]
	v_pk_add_f32 v[28:29], v[46:47], v[28:29] neg_lo:[0,1] neg_hi:[0,1]
	v_pk_mul_f32 v[50:51], v[90:91], v[32:33] op_sel:[0,1] op_sel_hi:[0,0] neg_lo:[0,1]
	v_pk_fma_f32 v[86:87], v[86:87], v[32:33], v[50:51] op_sel_hi:[0,1,1] neg_lo:[1,0,0] neg_hi:[1,0,0]
	v_pk_mul_f32 v[32:33], v[92:93], v[28:29] op_sel:[0,1] op_sel_hi:[0,0] neg_lo:[0,1]
	v_pk_fma_f32 v[46:47], v[84:85], v[28:29], v[32:33] op_sel_hi:[0,1,1] neg_lo:[1,0,0] neg_hi:[1,0,0]
	v_pk_add_f32 v[28:29], v[44:45], v[26:27]
	v_pk_add_f32 v[26:27], v[44:45], v[26:27] neg_lo:[0,1] neg_hi:[0,1]
	v_pk_add_f32 v[50:51], v[66:67], v[42:43]
	v_pk_mul_f32 v[32:33], v[94:95], v[26:27] op_sel:[0,1] op_sel_hi:[0,0] neg_lo:[0,1]
	v_pk_fma_f32 v[90:91], v[10:11], v[26:27], v[32:33] op_sel_hi:[0,1,1] neg_lo:[1,0,0] neg_hi:[1,0,0]
	v_pk_add_f32 v[32:33], v[96:97], v[48:49] neg_lo:[0,1] neg_hi:[0,1]
	v_pk_add_f32 v[26:27], v[96:97], v[48:49]
	v_pk_mul_f32 v[44:45], v[92:93], v[32:33] op_sel:[0,1] op_sel_hi:[0,0] neg_lo:[0,1]
	v_pk_fma_f32 v[48:49], v[84:85], v[32:33], v[44:45] op_sel_hi:[0,1,1]
	v_pk_add_f32 v[32:33], v[66:67], v[42:43] neg_lo:[0,1] neg_hi:[0,1]
	v_pk_add_f32 v[44:45], v[78:79], v[60:61] neg_lo:[0,1] neg_hi:[0,1]
	v_pk_mul_f32 v[42:43], v[88:89], v[32:33] op_sel:[0,1] op_sel_hi:[0,0] neg_lo:[0,1]
	v_pk_fma_f32 v[32:33], v[88:89], v[32:33], v[42:43] op_sel_hi:[0,1,1]
	v_pk_add_f32 v[42:43], v[78:79], v[60:61]
	v_pk_mul_f32 v[60:61], v[84:85], v[44:45] op_sel:[0,1] op_sel_hi:[0,0] neg_lo:[0,1]
	v_pk_add_f32 v[78:79], v[74:75], v[36:37]
	v_pk_add_f32 v[36:37], v[74:75], v[36:37] neg_lo:[0,1] neg_hi:[0,1]
	v_pk_fma_f32 v[68:69], v[92:93], v[44:45], v[60:61] op_sel_hi:[0,1,1]
	v_pk_mul_f32 v[44:45], v[84:85], v[36:37] op_sel:[0,1] op_sel_hi:[0,0] neg_lo:[0,1]
	v_pk_fma_f32 v[74:75], v[92:93], v[36:37], v[44:45] op_sel_hi:[0,1,1] neg_lo:[1,0,0] neg_hi:[1,0,0]
	v_pk_add_f32 v[36:37], v[56:57], v[54:55] neg_lo:[0,1] neg_hi:[0,1]
	v_pk_add_f32 v[60:61], v[56:57], v[54:55]
	v_pk_mul_f32 v[44:45], v[88:89], v[36:37] op_sel:[0,1] op_sel_hi:[0,0] neg_lo:[0,1]
	v_pk_fma_f32 v[44:45], v[88:89], v[36:37], v[44:45] op_sel_hi:[0,1,1] neg_lo:[1,0,0] neg_hi:[1,0,0]
	v_pk_add_f32 v[36:37], v[70:71], v[28:29]
	v_pk_add_f32 v[28:29], v[70:71], v[28:29] neg_lo:[0,1] neg_hi:[0,1]
	v_pk_add_f32 v[66:67], v[26:27], v[78:79]
	v_pk_mul_f32 v[54:55], v[92:93], v[28:29] op_sel:[0,1] op_sel_hi:[0,0] neg_lo:[0,1]
	v_pk_add_f32 v[26:27], v[26:27], v[78:79] neg_lo:[0,1] neg_hi:[0,1]
	v_pk_fma_f32 v[94:95], v[84:85], v[28:29], v[54:55] op_sel_hi:[0,1,1] neg_lo:[1,0,0] neg_hi:[1,0,0]
	v_pk_mul_f32 v[28:29], v[88:89], v[26:27] op_sel:[0,1] op_sel_hi:[0,0] neg_lo:[0,1]
	v_pk_fma_f32 v[26:27], v[88:89], v[26:27], v[28:29] op_sel_hi:[0,1,1]
	v_pk_add_f32 v[28:29], v[42:43], v[36:37] neg_lo:[0,1] neg_hi:[0,1]
	v_pk_add_f32 v[70:71], v[42:43], v[36:37]
	v_pk_mul_f32 v[36:37], v[88:89], v[28:29] op_sel:[0,1] op_sel_hi:[0,0] neg_lo:[0,1]
	v_pk_fma_f32 v[36:37], v[88:89], v[28:29], v[36:37] op_sel_hi:[0,1,1] neg_lo:[1,0,0] neg_hi:[1,0,0]
	v_pk_add_f32 v[28:29], v[48:49], v[74:75] neg_lo:[0,1] neg_hi:[0,1]
	v_pk_add_f32 v[54:55], v[48:49], v[74:75]
	v_pk_mul_f32 v[42:43], v[88:89], v[28:29] op_sel:[0,1] op_sel_hi:[0,0] neg_lo:[0,1]
	v_pk_fma_f32 v[28:29], v[88:89], v[28:29], v[42:43] op_sel_hi:[0,1,1]
	v_pk_add_f32 v[42:43], v[68:69], v[94:95] neg_lo:[0,1] neg_hi:[0,1]
	v_pk_add_f32 v[74:75], v[80:81], v[62:63]
	v_pk_mul_f32 v[48:49], v[88:89], v[42:43] op_sel:[0,1] op_sel_hi:[0,0] neg_lo:[0,1]
	v_pk_fma_f32 v[42:43], v[88:89], v[42:43], v[48:49] op_sel_hi:[0,1,1] neg_lo:[1,0,0] neg_hi:[1,0,0]
	v_pk_add_f32 v[48:49], v[80:81], v[62:63] neg_lo:[0,1] neg_hi:[0,1]
	v_pk_add_f32 v[56:57], v[68:69], v[94:95]
	v_pk_mul_f32 v[62:63], v[92:93], v[48:49] op_sel:[0,1] op_sel_hi:[0,0] neg_lo:[0,1]
	v_pk_fma_f32 v[94:95], v[84:85], v[48:49], v[62:63] op_sel_hi:[0,1,1]
	v_pk_add_f32 v[48:49], v[64:65], v[100:101] neg_lo:[0,1] neg_hi:[0,1]
	v_pk_add_f32 v[68:69], v[64:65], v[100:101]
	v_pk_mul_f32 v[62:63], v[88:89], v[48:49] op_sel:[0,1] op_sel_hi:[0,0] neg_lo:[0,1]
	v_pk_add_f32 v[64:65], v[76:77], v[58:59]
	v_pk_add_f32 v[58:59], v[76:77], v[58:59] neg_lo:[0,1] neg_hi:[0,1]
	v_pk_fma_f32 v[48:49], v[88:89], v[48:49], v[62:63] op_sel_hi:[0,1,1]
	v_pk_mul_f32 v[62:63], v[84:85], v[58:59] op_sel:[0,1] op_sel_hi:[0,0] neg_lo:[0,1]
	v_pk_fma_f32 v[96:97], v[92:93], v[58:59], v[62:63] op_sel_hi:[0,1,1]
	v_pk_add_f32 v[58:59], v[72:73], v[86:87] neg_lo:[0,1] neg_hi:[0,1]
	v_pk_add_f32 v[76:77], v[52:53], v[46:47]
	v_pk_add_f32 v[46:47], v[52:53], v[46:47] neg_lo:[0,1] neg_hi:[0,1]
	v_pk_add_f32 v[62:63], v[72:73], v[86:87]
	v_pk_mul_f32 v[72:73], v[84:85], v[58:59] op_sel:[0,1] op_sel_hi:[0,0] neg_lo:[0,1]
	v_pk_mul_f32 v[52:53], v[88:89], v[46:47] op_sel:[0,1] op_sel_hi:[0,0] neg_lo:[0,1]
	v_pk_fma_f32 v[86:87], v[92:93], v[58:59], v[72:73] op_sel_hi:[0,1,1] neg_lo:[1,0,0] neg_hi:[1,0,0]
	v_pk_fma_f32 v[58:59], v[88:89], v[46:47], v[52:53] op_sel_hi:[0,1,1] neg_lo:[1,0,0] neg_hi:[1,0,0]
	v_pk_add_f32 v[46:47], v[98:99], v[90:91]
	v_pk_add_f32 v[52:53], v[98:99], v[90:91] neg_lo:[0,1] neg_hi:[0,1]
	v_pk_add_f32 v[80:81], v[64:65], v[46:47]
	v_pk_add_f32 v[46:47], v[64:65], v[46:47] neg_lo:[0,1] neg_hi:[0,1]
	s_nop 0
	v_pk_mul_f32 v[64:65], v[88:89], v[46:47] op_sel:[0,1] op_sel_hi:[0,0] neg_lo:[0,1]
	v_pk_fma_f32 v[64:65], v[88:89], v[46:47], v[64:65] op_sel_hi:[0,1,1] neg_lo:[1,0,0] neg_hi:[1,0,0]
	v_pk_add_f32 v[46:47], v[94:95], v[86:87] neg_lo:[0,1] neg_hi:[0,1]
	v_pk_mul_f32 v[72:73], v[92:93], v[52:53] op_sel:[0,1] op_sel_hi:[0,0] neg_lo:[0,1]
	v_pk_add_f32 v[78:79], v[74:75], v[62:63]
	v_pk_add_f32 v[62:63], v[74:75], v[62:63] neg_lo:[0,1] neg_hi:[0,1]
	v_pk_fma_f32 v[52:53], v[84:85], v[52:53], v[72:73] op_sel_hi:[0,1,1] neg_lo:[1,0,0] neg_hi:[1,0,0]
	v_pk_mul_f32 v[74:75], v[88:89], v[46:47] op_sel:[0,1] op_sel_hi:[0,0] neg_lo:[0,1]
	v_pk_fma_f32 v[46:47], v[88:89], v[46:47], v[74:75] op_sel_hi:[0,1,1]
	v_pk_add_f32 v[74:75], v[96:97], v[52:53]
	v_pk_add_f32 v[52:53], v[96:97], v[52:53] neg_lo:[0,1] neg_hi:[0,1]
	v_add_f32_e32 v30, v30, v34
	v_pk_mul_f32 v[84:85], v[88:89], v[52:53] op_sel:[0,1] op_sel_hi:[0,0] neg_lo:[0,1]
	v_sub_f32_e32 v34, v16, v18
	v_sub_f32_e32 v13, v51, v61
	v_pk_fma_f32 v[52:53], v[88:89], v[52:53], v[84:85] op_sel_hi:[0,1,1] neg_lo:[1,0,0] neg_hi:[1,0,0]
	v_sub_f32_e32 v51, v34, v82
	v_sub_f32_e32 v25, v29, v43
	v_sub_f32_e32 v43, v31, v35
	v_sub_f32_e32 v35, v49, v59
	v_sub_f32_e32 v10, v47, v53
	v_add_f32_e32 v49, v50, v60
	v_add_f32_e32 v50, v68, v76
	v_add_f32_e32 v53, v51, v30
	v_sub_f32_e32 v23, v27, v37
	v_sub_f32_e32 v27, v55, v57
	v_add_f32_e32 v38, v38, v40
	v_add_f32_e32 v40, v78, v80
	v_add_f32_e32 v55, v53, v50
	v_add_f32_e32 v16, v55, v40
	v_sub_f32_e32 v41, v39, v41
	v_add_f32_e32 v21, v20, v38
	global_store_dword v[14:15], v16, off offset:2048
	v_add_co_u32_e32 v16, vcc, s10, v14
	v_add_f32_e32 v47, v66, v70
	v_add_f32_e32 v24, v21, v49
	v_add_f32_e32 v32, v32, v44
	v_sub_f32_e32 v44, v22, v41
	v_addc_co_u32_e32 v17, vcc, 0, v15, vcc
	v_pk_mul_f32 v[72:73], v[88:89], v[62:63] op_sel:[0,1] op_sel_hi:[0,0] neg_lo:[0,1]
	v_add_f32_e32 v19, v24, v47
	v_add_f32_e32 v54, v54, v56
	v_add_f32_e32 v56, v44, v32
	v_add_co_u32_e32 v18, vcc, s11, v14
	v_add_f32_e32 v34, v34, v82
	v_pk_fma_f32 v[62:63], v[88:89], v[62:63], v[72:73] op_sel_hi:[0,1,1]
	v_pk_add_f32 v[72:73], v[94:95], v[86:87]
	global_store_dword v[14:15], v19, off
	v_add_f32_e32 v57, v56, v54
	v_addc_co_u32_e32 v19, vcc, 0, v15, vcc
	v_add_f32_e32 v48, v48, v58
	v_sub_f32_e32 v58, v34, v43
	global_store_dword v[18:19], v57, off offset:-4096
	v_add_f32_e32 v57, v72, v74
	v_add_f32_e32 v59, v58, v48
	v_sub_f32_e32 v20, v20, v38
	v_sub_f32_e32 v37, v33, v45
	v_sub_f32_e32 v45, v69, v77
	v_add_f32_e32 v60, v59, v57
	v_add_f32_e32 v26, v26, v36
	v_sub_f32_e32 v36, v20, v13
	v_sub_f32_e32 v30, v51, v30
	global_store_dword v[16:17], v60, off offset:2048
	v_add_f32_e32 v16, v36, v26
	v_add_f32_e32 v38, v62, v64
	v_sub_f32_e32 v51, v30, v45
	global_store_dword v[18:19], v16, off
	v_add_f32_e32 v16, v51, v38
	global_store_dword v[18:19], v16, off offset:2048
	v_add_co_u32_e32 v16, vcc, s78, v14
	v_add_f32_e32 v22, v22, v41
	s_nop 0
	v_addc_co_u32_e32 v17, vcc, 0, v15, vcc
	v_add_f32_e32 v28, v28, v42
	v_sub_f32_e32 v41, v22, v37
	v_add_co_u32_e32 v18, vcc, s43, v14
	v_add_f32_e32 v42, v41, v28
	s_nop 0
	v_addc_co_u32_e32 v19, vcc, 0, v15, vcc
	v_add_f32_e32 v34, v34, v43
	global_store_dword v[18:19], v42, off offset:-4096
	v_add_f32_e32 v42, v46, v52
	v_sub_f32_e32 v43, v34, v35
	v_sub_f32_e32 v39, v67, v71
	v_add_f32_e32 v46, v43, v42
	v_sub_f32_e32 v21, v21, v49
	v_sub_f32_e32 v33, v79, v81
	global_store_dword v[16:17], v46, off offset:2048
	v_sub_f32_e32 v16, v21, v39
	v_sub_f32_e32 v46, v53, v50
	global_store_dword v[18:19], v16, off
	v_sub_f32_e32 v16, v46, v33
	global_store_dword v[18:19], v16, off offset:2048
	v_add_co_u32_e32 v16, vcc, s13, v14
	v_sub_f32_e32 v32, v44, v32
	s_nop 0
	v_addc_co_u32_e32 v17, vcc, 0, v15, vcc
	v_add_co_u32_e32 v18, vcc, s12, v14
	v_sub_f32_e32 v44, v32, v27
	s_nop 0
	v_addc_co_u32_e32 v19, vcc, 0, v15, vcc
	v_sub_f32_e32 v31, v73, v75
	global_store_dword v[18:19], v44, off offset:-4096
	v_sub_f32_e32 v44, v58, v48
	v_sub_f32_e32 v48, v44, v31
	v_add_f32_e32 v20, v20, v13
	v_sub_f32_e32 v29, v63, v65
	global_store_dword v[16:17], v48, off offset:2048
	v_sub_f32_e32 v13, v20, v23
	v_add_f32_e32 v30, v30, v45
	v_add_co_u32_e32 v16, vcc, s16, v14
	global_store_dword v[18:19], v13, off
	v_sub_f32_e32 v13, v30, v29
	v_addc_co_u32_e32 v17, vcc, 0, v15, vcc
	global_store_dword v[18:19], v13, off offset:2048
	v_add_f32_e32 v22, v22, v37
	v_add_co_u32_e32 v18, vcc, s8, v14
	v_sub_f32_e32 v13, v22, v25
	s_nop 0
	v_addc_co_u32_e32 v19, vcc, 0, v15, vcc
	global_store_dword v[18:19], v13, off offset:-4096
	v_add_f32_e32 v13, v34, v35
	v_sub_f32_e32 v34, v13, v10
	global_store_dword v[16:17], v34, off offset:2048
	v_sub_f32_e32 v16, v24, v47
	global_store_dword v[18:19], v16, off
	v_sub_f32_e32 v16, v55, v40
	global_store_dword v[18:19], v16, off offset:2048
	v_add_co_u32_e32 v16, vcc, s9, v14
	v_sub_f32_e32 v24, v56, v54
	s_nop 0
	v_addc_co_u32_e32 v17, vcc, 0, v15, vcc
	v_add_co_u32_e32 v18, vcc, s7, v14
	v_add_f32_e32 v10, v13, v10
	s_nop 0
	v_addc_co_u32_e32 v19, vcc, 0, v15, vcc
	global_store_dword v[18:19], v24, off offset:-4096
	v_sub_f32_e32 v24, v59, v57
	global_store_dword v[16:17], v24, off offset:2048
	v_sub_f32_e32 v16, v36, v26
	global_store_dword v[18:19], v16, off
	v_sub_f32_e32 v16, v51, v38
	global_store_dword v[18:19], v16, off offset:2048
	v_add_co_u32_e32 v16, vcc, s5, v14
	v_sub_f32_e32 v24, v41, v28
	s_nop 0
	v_addc_co_u32_e32 v17, vcc, 0, v15, vcc
	v_add_co_u32_e32 v18, vcc, s6, v14
	s_nop 1
	v_addc_co_u32_e32 v19, vcc, 0, v15, vcc
	global_store_dword v[18:19], v24, off offset:-4096
	v_sub_f32_e32 v24, v43, v42
	global_store_dword v[16:17], v24, off offset:2048
	v_add_f32_e32 v16, v21, v39
	global_store_dword v[18:19], v16, off
	v_add_f32_e32 v16, v46, v33
	global_store_dword v[18:19], v16, off offset:2048
	v_add_co_u32_e32 v16, vcc, s4, v14
	v_add_f32_e32 v21, v32, v27
	s_nop 0
	v_addc_co_u32_e32 v17, vcc, 0, v15, vcc
	v_add_co_u32_e32 v18, vcc, s1, v14
	s_nop 1
	v_addc_co_u32_e32 v19, vcc, 0, v15, vcc
	global_store_dword v[18:19], v21, off offset:-4096
	v_add_f32_e32 v21, v44, v31
	global_store_dword v[16:17], v21, off offset:2048
	v_add_f32_e32 v16, v20, v23
	global_store_dword v[18:19], v16, off
	v_add_f32_e32 v16, v30, v29
	v_add_co_u32_e32 v14, vcc, s0, v14
	global_store_dword v[18:19], v16, off offset:2048
	v_add_f32_e32 v16, v22, v25
	v_addc_co_u32_e32 v15, vcc, 0, v15, vcc
	global_store_dword v[14:15], v16, off
	global_store_dword v[14:15], v10, off offset:2048
	v_mov_b32_e32 v10, v183
	v_mov_b32_e32 v14, v184
	v_mov_b32_e32 v18, v182
	s_movk_i32 s0, 0xfe00
	v_sub_u32_e32 v13, 0x4000, v18
	v_cmp_eq_u32_e32 vcc, 0, v18
	v_cmp_eq_u32_e64 s[0:1], s0, v18
	v_cmp_eq_u32_e64 s[4:5], s48, v18
	v_cndmask_b32_e64 v20, v13, 0, vcc
	v_sub_u32_e32 v13, 0x3e00, v18
	v_cndmask_b32_e64 v22, v13, 0, s[0:1]
	v_sub_u32_e32 v13, 0x3c00, v18
	v_ashrrev_i32_e32 v21, 31, v20
	v_ashrrev_i32_e32 v23, 31, v22
	v_cndmask_b32_e64 v24, v13, 0, s[4:5]
	v_lshl_add_u64 v[20:21], v[20:21], 1, s[2:3]
	v_lshl_add_u64 v[22:23], v[22:23], 1, s[2:3]
	v_ashrrev_i32_e32 v25, 31, v24
	v_sub_u32_e32 v13, 0x3a00, v18
	v_cmp_eq_u32_e64 s[6:7], s49, v18
	v_lshl_add_u64 v[24:25], v[24:25], 1, s[2:3]
	global_load_ushort v15, v[20:21], off
	s_nop 0
	global_load_ushort v22, v[22:23], off
	s_nop 0
	global_load_ushort v23, v[24:25], off
	v_cndmask_b32_e64 v20, v13, 0, s[6:7]
	v_ashrrev_i32_e32 v21, 31, v20
	v_ashrrev_i32_e32 v19, 31, v18
	v_lshl_add_u64 v[20:21], v[20:21], 1, s[2:3]
	v_lshl_add_u64 v[16:17], v[18:19], 1, s[76:77]
	global_load_ushort v20, v[20:21], off
	s_nop 0
	global_load_ushort v13, v[16:17], off offset:3072
	v_sub_u32_e32 v24, 0x3800, v18
	v_sub_u32_e32 v26, 0x3600, v18
	v_sub_u32_e32 v28, 0x3400, v18
	v_sub_u32_e32 v32, 0x3200, v18
	v_cmp_eq_u32_e64 s[8:9], s59, v18
	s_mov_b32 s48, s21
	s_mov_b32 s49, s20
	s_mov_b32 s59, s82
	s_waitcnt vmcnt(4)
	v_lshlrev_b32_e32 v15, 16, v15
	v_cndmask_b32_e64 v19, -v15, v15, vcc
	s_waitcnt vmcnt(3)
	v_lshlrev_b32_e32 v15, 16, v22
	v_cndmask_b32_e64 v31, -v15, v15, s[0:1]
	s_waitcnt vmcnt(2)
	v_lshlrev_b32_e32 v15, 16, v23
	v_cndmask_b32_e64 v30, -v15, v15, s[4:5]
	v_cmp_eq_u32_e64 s[4:5], s51, v18
	s_waitcnt vmcnt(1)
	v_lshlrev_b32_e32 v15, 16, v20
	v_add_co_u32_e32 v20, vcc, s10, v16
	v_cndmask_b32_e64 v15, -v15, v15, s[6:7]
	s_nop 0
	v_addc_co_u32_e32 v21, vcc, 0, v17, vcc
	v_add_co_u32_e32 v22, vcc, s11, v16
	v_cmp_eq_u32_e64 s[6:7], s50, v18
	s_nop 0
	v_addc_co_u32_e32 v23, vcc, 0, v17, vcc
	v_cmp_eq_u32_e64 s[0:1], s57, v18
	v_cndmask_b32_e64 v24, v24, 0, s[6:7]
	v_cndmask_b32_e64 v26, v26, 0, s[4:5]
	v_cndmask_b32_e64 v28, v28, 0, s[0:1]
	v_cmp_eq_u32_e32 vcc, s58, v18
	v_ashrrev_i32_e32 v25, 31, v24
	v_ashrrev_i32_e32 v27, 31, v26
	v_ashrrev_i32_e32 v29, 31, v28
	v_cndmask_b32_e64 v32, v32, 0, vcc
	v_lshl_add_u64 v[24:25], v[24:25], 1, s[2:3]
	v_lshl_add_u64 v[26:27], v[26:27], 1, s[2:3]
	v_lshl_add_u64 v[28:29], v[28:29], 1, s[2:3]
	v_ashrrev_i32_e32 v33, 31, v32
	v_lshl_add_u64 v[32:33], v[32:33], 1, s[2:3]
	global_load_ushort v34, v[24:25], off
	s_nop 0
	global_load_ushort v26, v[26:27], off
	s_nop 0
	global_load_ushort v27, v[28:29], off
	s_nop 0
	global_load_ushort v28, v[32:33], off
	v_sub_u32_e32 v24, 0x3000, v18
	v_cndmask_b32_e64 v24, v24, 0, s[8:9]
	v_ashrrev_i32_e32 v25, 31, v24
	v_lshl_add_u64 v[24:25], v[24:25], 1, s[2:3]
	global_load_ushort v24, v[24:25], off
	s_nop 0
	global_load_ushort v32, v[20:21], off offset:3072
	v_cmp_eq_u32_e64 s[10:11], s79, v18
	s_mov_b32 s79, s80
	s_waitcnt vmcnt(6)
	v_lshlrev_b32_e32 v13, 16, v13
	s_mov_b32 s57, s18
	s_mov_b32 s58, s83
	s_waitcnt vmcnt(5)
	v_lshlrev_b32_e32 v25, 16, v34
	v_cndmask_b32_e64 v33, -v25, v25, s[6:7]
	s_waitcnt vmcnt(4)
	v_lshlrev_b32_e32 v25, 16, v26
	v_cndmask_b32_e64 v34, -v25, v25, s[4:5]
	s_waitcnt vmcnt(3)
	v_lshlrev_b32_e32 v25, 16, v27
	v_cndmask_b32_e64 v35, -v25, v25, s[0:1]
	v_add_co_u32_e64 v26, s[0:1], s78, v16
	s_waitcnt vmcnt(2)
	v_lshlrev_b32_e32 v25, 16, v28
	s_waitcnt vmcnt(1)
	v_lshlrev_b32_e32 v24, 16, v24
	v_addc_co_u32_e64 v27, s[0:1], 0, v17, s[0:1]
	v_cndmask_b32_e64 v36, -v25, v25, vcc
	v_cndmask_b32_e64 v37, -v24, v24, s[8:9]
	v_sub_u32_e32 v24, 0x2e00, v18
	v_cmp_eq_u32_e32 vcc, s60, v18
	v_sub_u32_e32 v28, 0x2c00, v18
	v_cmp_eq_u32_e64 s[0:1], s61, v18
	v_cndmask_b32_e64 v24, v24, 0, vcc
	v_ashrrev_i32_e32 v25, 31, v24
	v_cndmask_b32_e64 v28, v28, 0, s[0:1]
	v_ashrrev_i32_e32 v29, 31, v28
	v_lshl_add_u64 v[24:25], v[24:25], 1, s[2:3]
	v_lshl_add_u64 v[28:29], v[28:29], 1, s[2:3]
	global_load_ushort v41, v[24:25], off
	s_nop 0
	global_load_ushort v28, v[28:29], off
	v_sub_u32_e32 v24, 0x2a00, v18
	v_cmp_eq_u32_e64 s[4:5], s62, v18
	v_cmp_eq_u32_e64 s[6:7], s63, v18
	v_cmp_eq_u32_e64 s[8:9], s68, v18
	v_cndmask_b32_e64 v24, v24, 0, s[4:5]
	v_ashrrev_i32_e32 v25, 31, v24
	v_lshl_add_u64 v[24:25], v[24:25], 1, s[2:3]
	global_load_ushort v29, v[24:25], off
	v_sub_u32_e32 v24, 0x2800, v18
	v_cndmask_b32_e64 v24, v24, 0, s[6:7]
	v_ashrrev_i32_e32 v25, 31, v24
	v_lshl_add_u64 v[24:25], v[24:25], 1, s[2:3]
	global_load_ushort v38, v[26:27], off offset:1024
	global_load_ushort v40, v[26:27], off offset:2048
	global_load_ushort v39, v[26:27], off offset:3072
	global_load_ushort v44, v[24:25], off
	v_sub_u32_e32 v26, 0x2600, v18
	s_mov_b32 s78, s81
	s_mov_b32 s60, s87
	s_mov_b32 s61, s86
	s_mov_b32 s68, s89
	s_mov_b32 s62, s93
	s_mov_b32 s63, s92
	s_waitcnt vmcnt(6)
	v_lshlrev_b32_e32 v24, 16, v41
	v_cndmask_b32_e64 v43, -v24, v24, vcc
	s_waitcnt vmcnt(5)
	v_lshlrev_b32_e32 v24, 16, v28
	v_cndmask_b32_e64 v41, -v24, v24, s[0:1]
	v_add_co_u32_e64 v28, s[0:1], s13, v16
	s_waitcnt vmcnt(4)
	v_lshlrev_b32_e32 v24, 16, v29
	v_cndmask_b32_e64 v42, -v24, v24, s[4:5]
	v_add_co_u32_e32 v24, vcc, s43, v16
	v_addc_co_u32_e64 v29, s[0:1], 0, v17, s[0:1]
	s_nop 0
	v_addc_co_u32_e32 v25, vcc, 0, v17, vcc
	v_cmp_eq_u32_e32 vcc, s66, v18
	v_cmp_eq_u32_e64 s[4:5], s74, v18
	v_cmp_eq_u32_e64 s[0:1], s75, v18
	v_cndmask_b32_e64 v26, v26, 0, vcc
	v_ashrrev_i32_e32 v27, 31, v26
	v_lshl_add_u64 v[26:27], v[26:27], 1, s[2:3]
	global_load_ushort v26, v[26:27], off
	s_waitcnt vmcnt(1)
	v_lshlrev_b32_e32 v27, 16, v44
	v_sub_u32_e32 v44, 0x2200, v18
	v_cndmask_b32_e64 v45, -v27, v27, s[6:7]
	v_cndmask_b32_e64 v46, v44, 0, s[8:9]
	v_sub_u32_e32 v44, 0x2000, v18
	v_cmp_eq_u32_e64 s[6:7], s69, v18
	v_ashrrev_i32_e32 v47, 31, v46
	v_lshl_add_u64 v[46:47], v[46:47], 1, s[2:3]
	v_cndmask_b32_e64 v50, v44, 0, s[6:7]
	v_sub_u32_e32 v44, 0x1e00, v18
	v_cndmask_b32_e64 v52, v44, 0, s[4:5]
	v_sub_u32_e32 v44, 0x1c00, v18
	v_ashrrev_i32_e32 v51, 31, v50
	v_cndmask_b32_e64 v54, v44, 0, s[0:1]
	v_lshl_add_u64 v[50:51], v[50:51], 1, s[2:3]
	v_ashrrev_i32_e32 v53, 31, v52
	v_ashrrev_i32_e32 v55, 31, v54
	v_lshl_add_u64 v[52:53], v[52:53], 1, s[2:3]
	v_lshl_add_u64 v[54:55], v[54:55], 1, s[2:3]
	s_mov_b32 s66, s25
	s_mov_b32 s69, s88
	s_mov_b32 s74, s29
	s_mov_b32 s75, s28
	s_movk_i32 s43, 0x6000
	s_waitcnt vmcnt(0)
	v_lshlrev_b32_e32 v26, 16, v26
	v_cndmask_b32_e64 v49, -v26, v26, vcc
	v_sub_u32_e32 v26, 0x2400, v18
	v_cmp_eq_u32_e32 vcc, s67, v18
	s_mov_b32 s67, s24
	s_nop 0
	v_cndmask_b32_e64 v26, v26, 0, vcc
	v_ashrrev_i32_e32 v27, 31, v26
	v_lshl_add_u64 v[26:27], v[26:27], 1, s[2:3]
	global_load_ushort v44, v[26:27], off
	s_nop 0
	global_load_ushort v46, v[46:47], off
	s_nop 0
	global_load_ushort v47, v[50:51], off
	global_load_ushort v48, v[52:53], off
	s_nop 0
	global_load_ushort v50, v[54:55], off
	v_sub_u32_e32 v26, 0x1a00, v18
	v_cndmask_b32_e64 v26, v26, 0, s[10:11]
	v_ashrrev_i32_e32 v27, 31, v26
	v_lshl_add_u64 v[26:27], v[26:27], 1, s[2:3]
	global_load_ushort v26, v[26:27], off
	s_nop 0
	global_load_ushort v53, v[28:29], off offset:1024
	global_load_ushort v51, v[28:29], off offset:2048
	s_waitcnt vmcnt(7)
	v_lshlrev_b32_e32 v27, 16, v44
	v_cndmask_b32_e64 v61, -v27, v27, vcc
	s_waitcnt vmcnt(6)
	v_lshlrev_b32_e32 v27, 16, v46
	v_cndmask_b32_e64 v63, -v27, v27, s[8:9]
	s_waitcnt vmcnt(5)
	v_lshlrev_b32_e32 v27, 16, v47
	v_cndmask_b32_e64 v90, -v27, v27, s[6:7]
	s_waitcnt vmcnt(4)
	v_lshlrev_b32_e32 v27, 16, v48
	v_cndmask_b32_e64 v59, -v27, v27, s[4:5]
	s_waitcnt vmcnt(3)
	v_lshlrev_b32_e32 v27, 16, v50
	v_cndmask_b32_e64 v57, -v27, v27, s[0:1]
	v_sub_u32_e32 v44, 0x1800, v18
	v_cmp_eq_u32_e64 s[8:9], s56, v18
	s_movk_i32 s0, 0xd600
	s_waitcnt vmcnt(2)
	v_lshlrev_b32_e32 v26, 16, v26
	v_cndmask_b32_e64 v46, v44, 0, s[8:9]
	v_sub_u32_e32 v44, 0x1600, v18
	v_cmp_eq_u32_e64 s[6:7], s0, v18
	s_movk_i32 s0, 0xd400
	v_cndmask_b32_e64 v55, -v26, v26, s[10:11]
	v_add_co_u32_e32 v26, vcc, s12, v16
	v_cndmask_b32_e64 v64, v44, 0, s[6:7]
	v_sub_u32_e32 v44, 0x1400, v18
	v_cmp_eq_u32_e64 s[4:5], s0, v18
	s_movk_i32 s0, 0xd200
	v_addc_co_u32_e32 v27, vcc, 0, v17, vcc
	v_cndmask_b32_e64 v66, v44, 0, s[4:5]
	v_sub_u32_e32 v44, 0x1200, v18
	v_cmp_eq_u32_e64 s[0:1], s0, v18
	s_movk_i32 s10, 0xd000
	v_cmp_eq_u32_e32 vcc, s10, v18
	v_cndmask_b32_e64 v68, v44, 0, s[0:1]
	v_sub_u32_e32 v44, 0x1000, v18
	v_ashrrev_i32_e32 v47, 31, v46
	v_cndmask_b32_e64 v70, v44, 0, vcc
	v_lshl_add_u64 v[46:47], v[46:47], 1, s[2:3]
	v_ashrrev_i32_e32 v65, 31, v64
	v_ashrrev_i32_e32 v67, 31, v66
	v_ashrrev_i32_e32 v69, 31, v68
	v_ashrrev_i32_e32 v71, 31, v70
	v_lshl_add_u64 v[64:65], v[64:65], 1, s[2:3]
	v_lshl_add_u64 v[66:67], v[66:67], 1, s[2:3]
	v_lshl_add_u64 v[68:69], v[68:69], 1, s[2:3]
	v_lshl_add_u64 v[70:71], v[70:71], 1, s[2:3]
	global_load_ushort v44, v[46:47], off
	global_load_ushort v48, v[64:65], off
	global_load_ushort v50, v[66:67], off
	global_load_ushort v52, v[68:69], off
	global_load_ushort v54, v[70:71], off
	v_sub_u32_e32 v46, 0xe00, v18
	v_cmp_eq_u32_e64 s[12:13], s84, v18
	s_movk_i32 s10, 0xcc00
	v_cmp_eq_u32_e64 s[10:11], s10, v18
	v_cndmask_b32_e64 v46, v46, 0, s[12:13]
	v_ashrrev_i32_e32 v47, 31, v46
	v_lshl_add_u64 v[46:47], v[46:47], 1, s[2:3]
	global_load_ushort v56, v[46:47], off
	v_sub_u32_e32 v46, 0xc00, v18
	v_cndmask_b32_e64 v46, v46, 0, s[10:11]
	v_ashrrev_i32_e32 v47, 31, v46
	v_lshl_add_u64 v[46:47], v[46:47], 1, s[2:3]
	global_load_ushort v46, v[46:47], off
	s_nop 0
	global_load_ushort v91, v[28:29], off offset:3072
	s_mov_b32 s84, 0x3f3504f3
	s_mov_b32 s85, 0xbf3504f3
	s_mov_b32 s54, s85
	s_mov_b32 s55, s84
	s_mov_b32 s56, s19
	s_mov_b32 s38, s85
	s_waitcnt vmcnt(7)
	v_lshlrev_b32_e32 v28, 16, v44
	v_cndmask_b32_e64 v97, -v28, v28, s[8:9]
	s_waitcnt vmcnt(6)
	v_lshlrev_b32_e32 v28, 16, v48
	v_cndmask_b32_e64 v96, -v28, v28, s[6:7]
	s_waitcnt vmcnt(5)
	v_lshlrev_b32_e32 v28, 16, v50
	v_cndmask_b32_e64 v94, -v28, v28, s[4:5]
	s_waitcnt vmcnt(4)
	v_lshlrev_b32_e32 v28, 16, v52
	v_cndmask_b32_e64 v93, -v28, v28, s[0:1]
	s_waitcnt vmcnt(3)
	v_lshlrev_b32_e32 v28, 16, v54
	v_cndmask_b32_e64 v92, -v28, v28, vcc
	s_movk_i32 s0, 0xca00
	v_cmp_eq_u32_e64 s[0:1], s0, v18
	s_waitcnt vmcnt(2)
	v_lshlrev_b32_e32 v28, 16, v56
	v_cndmask_b32_e64 v95, -v28, v28, s[12:13]
	v_sub_u32_e32 v28, 0xa00, v18
	v_cndmask_b32_e64 v28, v28, 0, s[0:1]
	v_ashrrev_i32_e32 v29, 31, v28
	v_lshl_add_u64 v[28:29], v[28:29], 1, s[2:3]
	global_load_ushort v44, v[28:29], off
	s_waitcnt vmcnt(2)
	v_lshlrev_b32_e32 v28, 16, v46
	v_cndmask_b32_e64 v106, -v28, v28, s[10:11]
	v_add_co_u32_e32 v28, vcc, s16, v16
	s_movk_i32 s4, 0xc400
	s_nop 0
	v_addc_co_u32_e32 v29, vcc, 0, v17, vcc
	v_sub_u32_e32 v46, 0x400, v18
	v_cmp_eq_u32_e32 vcc, s4, v18
	s_movk_i32 s4, 0xc800
	v_sub_u32_e32 v48, 0x800, v18
	v_cndmask_b32_e64 v46, v46, 0, vcc
	v_cmp_eq_u32_e64 s[4:5], s4, v18
	v_ashrrev_i32_e32 v47, 31, v46
	v_lshl_add_u64 v[46:47], v[46:47], 1, s[2:3]
	v_cndmask_b32_e64 v64, v48, 0, s[4:5]
	v_ashrrev_i32_e32 v65, 31, v64
	v_lshl_add_u64 v[64:65], v[64:65], 1, s[2:3]
	global_load_ushort v48, v[46:47], off
	s_nop 0
	global_load_ushort v46, v[64:65], off
	global_load_ushort v110, v[28:29], off
	global_load_ushort v112, v[28:29], off offset:1024
	global_load_ushort v114, v[28:29], off offset:2048
	global_load_ushort v116, v[28:29], off offset:3072
	s_mov_b32 s6, 0x3f7b14be
	s_mov_b32 s7, 0xbe47c5c2
	s_mov_b32 s16, 0x3f6c835e
	s_mov_b32 s17, 0xbec3ef15
	s_mov_b32 s50, s17
	s_mov_b32 s51, s16
	v_add_f32_e32 v50, v15, v13
	s_mov_b32 s8, 0x3e47c5c2
	s_mov_b32 s9, 0xbf7b14be
	s_mov_b32 s30, s9
	s_mov_b32 s31, s8
	s_mov_b32 s10, s93
	s_mov_b32 s11, s81
	s_mov_b32 s12, s17
	s_mov_b32 s13, s19
	s_waitcnt vmcnt(6)
	v_lshlrev_b32_e32 v28, 16, v44
	v_cndmask_b32_e64 v108, -v28, v28, s[0:1]
	s_movk_i32 s0, 0xc600
	v_sub_u32_e32 v28, 0x600, v18
	v_sub_u32_e32 v44, 0x200, v18
	s_waitcnt vmcnt(4)
	v_lshlrev_b32_e32 v29, 16, v46
	v_cndmask_b32_e64 v111, -v29, v29, s[4:5]
	v_cmp_eq_u32_e64 s[4:5], s0, v18
	s_movk_i32 s0, 0xc200
	v_cmp_eq_u32_e64 s[0:1], s0, v18
	v_cndmask_b32_e64 v28, v28, 0, s[4:5]
	v_ashrrev_i32_e32 v29, 31, v28
	v_cndmask_b32_e64 v46, v44, 0, s[0:1]
	v_lshl_add_u64 v[28:29], v[28:29], 1, s[2:3]
	v_ashrrev_i32_e32 v47, 31, v46
	v_lshl_add_u64 v[46:47], v[46:47], 1, s[2:3]
	global_load_ushort v18, v[16:17], off
	s_nop 0
	global_load_ushort v28, v[28:29], off
	s_nop 0
	global_load_ushort v29, v[16:17], off offset:1024
	s_nop 0
	global_load_ushort v17, v[16:17], off offset:2048
	s_nop 0
	global_load_ushort v44, v[46:47], off
	global_load_ushort v58, v[22:23], off offset:1024
	global_load_ushort v62, v[22:23], off offset:2048
	global_load_ushort v68, v[22:23], off offset:3072
	global_load_ushort v69, v[24:25], off offset:-4096
	global_load_ushort v98, v[24:25], off
	global_load_ushort v52, v[22:23], off offset:-4096
	global_load_ushort v54, v[20:21], off offset:1024
	s_nop 0
	global_load_ushort v21, v[20:21], off offset:2048
	s_nop 0
	global_load_ushort v56, v[22:23], off
	s_mov_b32 s2, 0x3f7ec46d
	s_mov_b32 s3, 0xbdc8bd36
	v_lshlrev_b32_e32 v22, 16, v48
	s_mov_b32 s76, s3
	s_mov_b32 s77, s2
	v_cndmask_b32_e64 v115, -v22, v22, vcc
	v_pk_mul_f32 v[22:23], v[14:15], s[76:77] op_sel_hi:[0,1] neg_lo:[1,0]
	s_mov_b64 vcc, s[64:65]
	s_mov_b32 s64, s7
	s_mov_b32 s65, s6
	s_waitcnt vmcnt(13)
	v_lshlrev_b32_e32 v16, 16, v18
	s_waitcnt vmcnt(12)
	v_lshlrev_b32_e32 v18, 16, v28
	s_waitcnt vmcnt(11)
	v_lshlrev_b32_e32 v20, 16, v29
	s_waitcnt vmcnt(10)
	v_lshlrev_b32_e32 v17, 16, v17
	v_add_f32_e32 v20, v31, v20
	v_pk_fma_f32 v[28:29], v[10:11], s[2:3], v[22:23] op_sel_hi:[0,1,1]
	v_add_f32_e32 v22, v30, v17
	v_pk_mul_f32 v[30:31], v[14:15], s[64:65] op_sel_hi:[0,1] neg_lo:[1,0]
	v_pk_fma_f32 v[46:47], v[10:11], s[6:7], v[30:31] op_sel_hi:[0,1,1]
	v_pk_mul_f32 v[30:31], v[14:15], s[78:79] op_sel_hi:[0,1] neg_lo:[1,0]
	v_pk_fma_f32 v[88:89], v[10:11], s[80:81], v[30:31] op_sel_hi:[0,1,1]
	s_waitcnt vmcnt(3)
	v_lshlrev_b32_e32 v13, 16, v52
	v_pk_mul_f32 v[30:31], v[14:15], s[50:51] op_sel_hi:[0,1] neg_lo:[1,0]
	v_add_f32_e32 v16, v19, v16
	v_cndmask_b32_e64 v113, -v18, v18, s[4:5]
	v_pk_mul_f32 v[18:19], v[14:15], s[40:41] op_sel_hi:[0,1] neg_lo:[1,0]
	v_add_f32_e32 v52, v33, v13
	v_pk_fma_f32 v[84:85], v[10:11], s[16:17], v[30:31] op_sel_hi:[0,1,1]
	s_waitcnt vmcnt(2)
	v_lshlrev_b32_e32 v13, 16, v54
	v_pk_mul_f32 v[30:31], v[14:15], s[48:49] op_sel_hi:[0,1] neg_lo:[1,0]
	s_waitcnt vmcnt(1)
	v_lshlrev_b32_e32 v15, 16, v21
	v_lshlrev_b32_e32 v17, 16, v44
	v_add_f32_e32 v44, v34, v13
	global_load_ushort v13, v[24:25], off offset:1024
	global_load_ushort v33, v[26:27], off
	v_add_f32_e32 v48, v35, v15
	global_load_ushort v15, v[24:25], off offset:2048
	v_lshlrev_b32_e32 v21, 16, v32
	s_waitcnt vmcnt(3)
	v_lshlrev_b32_e32 v23, 16, v56
	v_add_f32_e32 v54, v36, v21
	global_load_ushort v21, v[24:25], off offset:3072
	v_add_f32_e32 v56, v37, v23
	v_lshlrev_b32_e32 v23, 16, v58
	v_add_f32_e32 v60, v43, v23
	global_load_ushort v23, v[26:27], off offset:-4096
	v_pk_fma_f32 v[64:65], v[10:11], s[20:21], v[30:31] op_sel_hi:[0,1,1]
	s_mov_b32 s4, 0x3dc8bd36
	s_mov_b32 s5, 0xbf7ec46d
	s_mov_b32 s34, s5
	s_mov_b32 s35, s4
	s_mov_b32 s2, s5
	v_cndmask_b32_e64 v17, -v17, v17, s[0:1]
	s_mov_b32 s0, s3
	s_mov_b32 s1, s5
	s_mov_b32 s6, s9
	s_mov_b32 s16, s19
	s_mov_b32 s20, s89
	v_pk_fma_f32 v[18:19], v[10:11], s[44:45], v[18:19] op_sel_hi:[0,1,1]
	s_waitcnt vmcnt(4)
	v_lshlrev_b32_e32 v13, 16, v13
	s_waitcnt vmcnt(2)
	v_pk_mul_f32 v[24:25], v[14:15], s[54:55] op_sel_hi:[0,1] neg_lo:[1,0]
	v_pk_fma_f32 v[78:79], v[10:11], s[84:85], v[24:25] op_sel_hi:[0,1,1]
	v_pk_mul_f32 v[24:25], v[14:15], s[60:61] op_sel_hi:[0,1] neg_lo:[1,0]
	v_pk_fma_f32 v[86:87], v[10:11], s[86:87], v[24:25] op_sel_hi:[0,1,1]
	v_lshlrev_b32_e32 v24, 16, v62
	v_add_f32_e32 v62, v41, v24
	v_pk_mul_f32 v[24:25], v[14:15], s[66:67] op_sel_hi:[0,1] neg_lo:[1,0]
	v_pk_fma_f32 v[82:83], v[10:11], s[24:25], v[24:25] op_sel_hi:[0,1,1]
	v_lshlrev_b32_e32 v24, 16, v68
	v_add_f32_e32 v58, v42, v24
	v_pk_mul_f32 v[24:25], v[14:15], s[68:69] op_sel_hi:[0,1] neg_lo:[1,0]
	v_pk_fma_f32 v[80:81], v[10:11], s[88:89], v[24:25] op_sel_hi:[0,1,1]
	v_lshlrev_b32_e32 v24, 16, v69
	v_add_f32_e32 v42, v45, v24
	v_pk_mul_f32 v[24:25], v[14:15], s[56:57] op_sel_hi:[0,1] neg_lo:[1,0]
	v_pk_fma_f32 v[74:75], v[10:11], s[18:19], v[24:25] op_sel_hi:[0,1,1]
	v_lshlrev_b32_e32 v24, 16, v38
	v_add_f32_e32 v38, v49, v24
	v_pk_mul_f32 v[24:25], v[14:15], s[62:63] op_sel_hi:[0,1] neg_lo:[1,0]
	v_pk_fma_f32 v[72:73], v[10:11], s[92:93], v[24:25] op_sel_hi:[0,1,1]
	v_lshlrev_b32_e32 v25, 16, v39
	v_add_f32_e32 v32, v63, v25
	global_load_ushort v25, v[26:27], off offset:1024
	global_load_ushort v39, v[26:27], off offset:2048
	v_lshlrev_b32_e32 v24, 16, v40
	global_load_ushort v40, v[26:27], off offset:3072
	v_pk_mul_f32 v[30:31], v[14:15], s[58:59] op_sel_hi:[0,1] neg_lo:[1,0]
	v_pk_fma_f32 v[66:67], v[10:11], s[82:83], v[30:31] op_sel_hi:[0,1,1]
	v_pk_mul_f32 v[30:31], v[14:15], s[74:75] op_sel_hi:[0,1] neg_lo:[1,0]
	v_pk_fma_f32 v[76:77], v[10:11], s[28:29], v[30:31] op_sel_hi:[0,1,1]
	v_pk_mul_f32 v[30:31], v[14:15], s[30:31] op_sel_hi:[0,1] neg_lo:[1,0]
	v_pk_fma_f32 v[68:69], v[10:11], s[8:9], v[30:31] op_sel_hi:[0,1,1]
	v_pk_mul_f32 v[30:31], v[14:15], s[34:35] op_sel_hi:[0,1] neg_lo:[1,0]
	v_pk_fma_f32 v[70:71], v[10:11], s[4:5], v[30:31] op_sel_hi:[0,1,1]
	v_lshlrev_b32_e32 v30, 16, v98
	v_pk_mul_f32 v[34:35], v[14:15], s[36:37] op_sel_hi:[0,1] neg_lo:[1,0]
	v_add_f32_e32 v30, v90, v30
	v_pk_fma_f32 v[34:35], v[10:11], s[96:97], v[34:35] op_sel_hi:[0,1,1]
	v_pk_mul_f32 v[36:37], v[34:35], v[30:31] op_sel_hi:[1,0]
	v_pk_mul_f32 v[30:31], v[14:15], s[2:3] op_sel_hi:[0,1] neg_lo:[1,0]
	v_add_f32_e32 v26, v59, v13
	v_pk_fma_f32 v[30:31], v[10:11], s[0:1], v[30:31] op_sel_hi:[0,1,1]
	v_lshlrev_b32_e32 v13, 16, v15
	s_mov_b32 s4, s7
	s_mov_b32 s5, s9
	v_pk_mul_f32 v[34:35], v[14:15], s[6:7] op_sel_hi:[0,1] neg_lo:[1,0]
	v_pk_mul_f32 v[26:27], v[30:31], v[26:27] op_sel_hi:[1,0]
	v_add_f32_e32 v30, v57, v13
	v_pk_fma_f32 v[34:35], v[10:11], s[4:5], v[34:35] op_sel_hi:[0,1,1]
	v_pk_mul_f32 v[98:99], v[34:35], v[30:31] op_sel_hi:[1,0]
	s_waitcnt vmcnt(4)
	v_lshlrev_b32_e32 v13, 16, v21
	s_mov_b32 s8, s81
	s_mov_b32 s9, s93
	v_pk_mul_f32 v[34:35], v[14:15], s[10:11] op_sel_hi:[0,1] neg_lo:[1,0]
	v_add_f32_e32 v30, v55, v13
	v_pk_fma_f32 v[34:35], v[10:11], s[8:9], v[34:35] op_sel_hi:[0,1,1]
	v_pk_mul_f32 v[100:101], v[34:35], v[30:31] op_sel_hi:[1,0]
	s_waitcnt vmcnt(3)
	v_lshlrev_b32_e32 v13, 16, v23
	v_pk_mul_f32 v[34:35], v[14:15], s[16:17] op_sel_hi:[0,1] neg_lo:[1,0]
	v_add_f32_e32 v30, v97, v13
	v_pk_fma_f32 v[34:35], v[10:11], s[12:13], v[34:35] op_sel_hi:[0,1,1]
	v_pk_mul_f32 v[102:103], v[34:35], v[30:31] op_sel_hi:[1,0]
	v_lshlrev_b32_e32 v13, 16, v53
	s_mov_b32 s18, s21
	s_mov_b32 s19, s89
	v_pk_mul_f32 v[34:35], v[14:15], s[20:21] op_sel_hi:[0,1] neg_lo:[1,0]
	v_add_f32_e32 v30, v96, v13
	v_pk_fma_f32 v[34:35], v[10:11], s[18:19], v[34:35] op_sel_hi:[0,1,1]
	s_mov_b32 s24, s25
	s_mov_b32 s25, s83
	v_pk_mul_f32 v[96:97], v[34:35], v[30:31] op_sel_hi:[1,0]
	v_lshlrev_b32_e32 v13, 16, v51
	v_pk_mul_f32 v[34:35], v[14:15], s[24:25] op_sel_hi:[0,1] neg_lo:[1,0]
	v_add_f32_e32 v30, v94, v13
	v_pk_fma_f32 v[34:35], v[10:11], s[22:23], v[34:35] op_sel_hi:[0,1,1]
	s_mov_b32 s28, s87
	v_pk_mul_f32 v[104:105], v[34:35], v[30:31] op_sel_hi:[1,0]
	v_lshlrev_b32_e32 v13, 16, v91
	v_pk_mul_f32 v[34:35], v[14:15], s[28:29] op_sel_hi:[0,1] neg_lo:[1,0]
	v_add_f32_e32 v30, v93, v13
	v_pk_fma_f32 v[34:35], v[10:11], s[26:27], v[34:35] op_sel_hi:[0,1,1]
	v_pk_mul_f32 v[90:91], v[34:35], v[30:31] op_sel_hi:[1,0]
	v_lshlrev_b32_e32 v13, 16, v33
	v_pk_mul_f32 v[34:35], v[14:15], s[84:85] op_sel_hi:[0,0] neg_lo:[1,0]
	v_add_f32_e32 v30, v92, v13
	v_pk_fma_f32 v[34:35], v[10:11], s[38:39], v[34:35] op_sel_hi:[0,0,1] neg_lo:[0,0,1] neg_hi:[0,0,1]
	v_pk_mul_f32 v[92:93], v[34:35], v[30:31] op_sel_hi:[1,0]
	v_pk_mul_f32 v[34:35], v[14:15], s[26:27] op_sel_hi:[0,1] neg_lo:[1,0]
	v_pk_fma_f32 v[34:35], v[10:11], s[28:29], v[34:35] op_sel_hi:[0,1,1]
	v_add_f32_e32 v24, v61, v24
	s_waitcnt vmcnt(2)
	v_lshlrev_b32_e32 v13, 16, v25
	v_add_f32_e32 v30, v95, v13
	v_pk_mul_f32 v[94:95], v[34:35], v[30:31] op_sel_hi:[1,0]
	s_waitcnt vmcnt(1)
	v_lshlrev_b32_e32 v13, 16, v39
	v_pk_mul_f32 v[34:35], v[14:15], s[22:23] op_sel_hi:[0,1] neg_lo:[1,0]
	v_add_f32_e32 v30, v106, v13
	v_pk_fma_f32 v[34:35], v[10:11], s[24:25], v[34:35] op_sel_hi:[0,1,1]
	v_pk_mul_f32 v[106:107], v[34:35], v[30:31] op_sel_hi:[1,0]
	s_waitcnt vmcnt(0)
	v_lshlrev_b32_e32 v13, 16, v40
	v_pk_mul_f32 v[34:35], v[14:15], s[18:19] op_sel_hi:[0,1] neg_lo:[1,0]
	v_add_f32_e32 v30, v108, v13
	v_pk_fma_f32 v[34:35], v[10:11], s[20:21], v[34:35] op_sel_hi:[0,1,1]
	v_pk_mul_f32 v[108:109], v[34:35], v[30:31] op_sel_hi:[1,0]
	v_lshlrev_b32_e32 v13, 16, v110
	v_pk_mul_f32 v[34:35], v[14:15], s[12:13] op_sel_hi:[0,1] neg_lo:[1,0]
	v_add_f32_e32 v30, v111, v13
	v_pk_fma_f32 v[34:35], v[10:11], s[16:17], v[34:35] op_sel_hi:[0,1,1]
	v_pk_mul_f32 v[110:111], v[34:35], v[30:31] op_sel_hi:[1,0]
	v_lshlrev_b32_e32 v13, 16, v112
	v_pk_mul_f32 v[34:35], v[14:15], s[8:9] op_sel_hi:[0,1] neg_lo:[1,0]
	v_add_f32_e32 v30, v113, v13
	v_pk_fma_f32 v[34:35], v[10:11], s[10:11], v[34:35] op_sel_hi:[0,1,1]
	v_pk_mul_f32 v[112:113], v[34:35], v[30:31] op_sel_hi:[1,0]
	v_lshlrev_b32_e32 v13, 16, v114
	v_pk_mul_f32 v[34:35], v[14:15], s[4:5] op_sel_hi:[0,1] neg_lo:[1,0]
	v_add_f32_e32 v30, v115, v13
	v_pk_fma_f32 v[34:35], v[10:11], s[6:7], v[34:35] op_sel_hi:[0,1,1]
	v_lshlrev_b32_e32 v13, 16, v116
	v_pk_mul_f32 v[14:15], v[14:15], s[0:1] op_sel_hi:[0,1] neg_lo:[1,0]
	v_pk_mul_f32 v[114:115], v[34:35], v[30:31] op_sel_hi:[1,0]
	v_add_f32_e32 v30, v17, v13
	v_pk_fma_f32 v[14:15], v[10:11], s[2:3], v[14:15] op_sel_hi:[0,1,1]
	v_pk_mul_f32 v[116:117], v[14:15], v[30:31] op_sel_hi:[1,0]
	v_mov_b32_e32 v13, v173
	v_mov_b32_e32 v10, v1
	v_mov_b32_e32 v30, v165
	v_mov_b32_e32 v10, v167
	v_mov_b32_e32 v34, v169
	v_mov_b32_e32 v17, v171
	s_nop 0
	v_pk_fma_f32 v[126:127], v[18:19], v[16:17], v[36:37] op_sel_hi:[1,0,1]
	v_pk_fma_f32 v[36:37], v[18:19], v[16:17], v[36:37] op_sel_hi:[1,0,1] neg_lo:[0,0,1] neg_hi:[0,0,1]
	v_pk_fma_f32 v[18:19], v[28:29], v[20:21], v[26:27] op_sel_hi:[1,0,1] neg_lo:[0,0,1] neg_hi:[0,0,1]
	v_pk_fma_f32 v[16:17], v[28:29], v[20:21], v[26:27] op_sel_hi:[1,0,1]
	v_pk_mul_f32 v[20:21], v[18:19], v[124:125] op_sel:[1,0] op_sel_hi:[0,0] neg_lo:[1,1] neg_hi:[0,1]
	s_nop 0
	v_pk_fma_f32 v[40:41], v[18:19], v[118:119], v[20:21] op_sel_hi:[1,0,1]
	v_pk_fma_f32 v[20:21], v[46:47], v[22:23], v[98:99] op_sel_hi:[1,0,1] neg_lo:[0,0,1] neg_hi:[0,0,1]
	v_pk_fma_f32 v[18:19], v[46:47], v[22:23], v[98:99] op_sel_hi:[1,0,1]
	v_pk_mul_f32 v[22:23], v[20:21], v[34:35] op_sel:[1,0] op_sel_hi:[0,0] neg_lo:[1,1] neg_hi:[0,1]
	s_nop 0
	v_pk_fma_f32 v[46:47], v[20:21], v[30:31], v[22:23] op_sel_hi:[1,0,1]
	v_pk_fma_f32 v[22:23], v[88:89], v[50:51], v[100:101] op_sel_hi:[1,0,1] neg_lo:[0,0,1] neg_hi:[0,0,1]
	v_pk_fma_f32 v[20:21], v[88:89], v[50:51], v[100:101] op_sel_hi:[1,0,1]
	v_pk_mul_f32 v[26:27], v[22:23], v[122:123] op_sel:[1,0] op_sel_hi:[0,0] neg_lo:[1,1] neg_hi:[0,1]
	s_nop 0
	v_pk_fma_f32 v[50:51], v[22:23], v[120:121], v[26:27] op_sel_hi:[1,0,1]
	v_pk_fma_f32 v[26:27], v[84:85], v[52:53], v[102:103] op_sel_hi:[1,0,1] neg_lo:[0,0,1] neg_hi:[0,0,1]
	v_pk_fma_f32 v[22:23], v[84:85], v[52:53], v[102:103] op_sel_hi:[1,0,1]
	v_pk_mul_f32 v[28:29], v[26:27], v[10:11] op_sel:[1,0] op_sel_hi:[0,0] neg_lo:[1,1] neg_hi:[0,1]
	s_nop 0
	v_pk_fma_f32 v[52:53], v[26:27], v[10:11], v[28:29] op_sel_hi:[1,0,1]
	v_pk_fma_f32 v[28:29], v[64:65], v[44:45], v[96:97] op_sel_hi:[1,0,1] neg_lo:[0,0,1] neg_hi:[0,0,1]
	v_pk_fma_f32 v[26:27], v[64:65], v[44:45], v[96:97] op_sel_hi:[1,0,1]
	v_pk_mul_f32 v[44:45], v[28:29], v[122:123] op_sel_hi:[1,0]
	s_nop 0
	v_pk_fma_f32 v[64:65], v[28:29], v[120:121], v[44:45] op_sel:[1,0,0] op_sel_hi:[0,0,1] neg_lo:[1,1,0] neg_hi:[0,1,0]
	v_pk_fma_f32 v[44:45], v[66:67], v[48:49], v[104:105] op_sel_hi:[1,0,1] neg_lo:[0,0,1] neg_hi:[0,0,1]
	v_pk_fma_f32 v[28:29], v[66:67], v[48:49], v[104:105] op_sel_hi:[1,0,1]
	v_pk_mul_f32 v[48:49], v[44:45], v[34:35] op_sel_hi:[1,0]
	s_nop 0
	v_pk_fma_f32 v[66:67], v[44:45], v[30:31], v[48:49] op_sel:[1,0,0] op_sel_hi:[0,0,1] neg_lo:[1,1,0] neg_hi:[0,1,0]
	v_pk_fma_f32 v[48:49], v[76:77], v[54:55], v[90:91] op_sel_hi:[1,0,1] neg_lo:[0,0,1] neg_hi:[0,0,1]
	v_pk_fma_f32 v[44:45], v[76:77], v[54:55], v[90:91] op_sel_hi:[1,0,1]
	v_pk_mul_f32 v[54:55], v[48:49], v[124:125] op_sel_hi:[1,0]
	v_xor_b32_e32 v76, 0x80000000, v49
	v_mov_b32_e32 v77, v48
	v_pk_fma_f32 v[48:49], v[78:79], v[56:57], v[92:93] op_sel_hi:[1,0,1]
	v_pk_fma_f32 v[56:57], v[78:79], v[56:57], v[92:93] op_sel_hi:[1,0,1] neg_lo:[0,0,1] neg_hi:[0,0,1]
	v_pk_fma_f32 v[54:55], v[76:77], v[118:119], v[54:55] op_sel_hi:[1,0,1] neg_lo:[0,1,0] neg_hi:[0,1,0]
	v_xor_b32_e32 v77, 0x80000000, v56
	v_mov_b32_e32 v76, v57
	v_pk_fma_f32 v[56:57], v[86:87], v[60:61], v[94:95] op_sel_hi:[1,0,1]
	v_pk_fma_f32 v[60:61], v[86:87], v[60:61], v[94:95] op_sel_hi:[1,0,1] neg_lo:[0,0,1] neg_hi:[0,0,1]
	s_nop 0
	v_pk_mul_f32 v[78:79], v[60:61], v[124:125] op_sel_hi:[1,0] neg_lo:[0,1] neg_hi:[0,1]
	s_nop 0
	v_pk_fma_f32 v[60:61], v[60:61], v[118:119], v[78:79] op_sel:[1,0,0] op_sel_hi:[0,0,1] neg_lo:[1,1,0] neg_hi:[0,1,0]
	v_pk_fma_f32 v[78:79], v[82:83], v[62:63], v[106:107] op_sel_hi:[1,0,1]
	v_pk_fma_f32 v[62:63], v[82:83], v[62:63], v[106:107] op_sel_hi:[1,0,1] neg_lo:[0,0,1] neg_hi:[0,0,1]
	s_nop 0
	v_pk_mul_f32 v[82:83], v[62:63], v[34:35] op_sel_hi:[1,0] neg_lo:[0,1] neg_hi:[0,1]
	s_nop 0
	v_pk_fma_f32 v[62:63], v[62:63], v[30:31], v[82:83] op_sel:[1,0,0] op_sel_hi:[0,0,1] neg_lo:[1,1,0] neg_hi:[0,1,0]
	v_pk_fma_f32 v[82:83], v[80:81], v[58:59], v[108:109] op_sel_hi:[1,0,1]
	v_pk_fma_f32 v[58:59], v[80:81], v[58:59], v[108:109] op_sel_hi:[1,0,1] neg_lo:[0,0,1] neg_hi:[0,0,1]
	s_nop 0
	v_pk_mul_f32 v[80:81], v[58:59], v[122:123] op_sel_hi:[1,0] neg_lo:[0,1] neg_hi:[0,1]
	s_nop 0
	v_pk_fma_f32 v[58:59], v[58:59], v[120:121], v[80:81] op_sel:[1,0,0] op_sel_hi:[0,0,1] neg_lo:[1,1,0] neg_hi:[0,1,0]
	v_pk_add_f32 v[84:85], v[16:17], v[56:57]
	v_pk_add_f32 v[16:17], v[16:17], v[56:57] neg_lo:[0,1] neg_hi:[0,1]
	v_pk_fma_f32 v[80:81], v[74:75], v[42:43], v[110:111] op_sel_hi:[1,0,1]
	v_pk_mul_f32 v[56:57], v[16:17], v[34:35] op_sel:[1,0] op_sel_hi:[0,0] neg_lo:[1,1] neg_hi:[0,1]
	v_pk_fma_f32 v[42:43], v[74:75], v[42:43], v[110:111] op_sel_hi:[1,0,1] neg_lo:[0,0,1] neg_hi:[0,0,1]
	v_pk_fma_f32 v[56:57], v[16:17], v[30:31], v[56:57] op_sel_hi:[1,0,1]
	v_pk_add_f32 v[16:17], v[18:19], v[78:79]
	v_pk_add_f32 v[18:19], v[18:19], v[78:79] neg_lo:[0,1] neg_hi:[0,1]
	v_pk_mul_f32 v[74:75], v[42:43], v[10:11] op_sel:[1,0] op_sel_hi:[0,0] neg_lo:[1,1] neg_hi:[0,1]
	v_pk_mul_f32 v[78:79], v[18:19], v[10:11] op_sel:[1,0] op_sel_hi:[0,0] neg_lo:[1,1] neg_hi:[0,1]
	v_pk_fma_f32 v[74:75], v[42:43], v[10:11], v[74:75] op_sel_hi:[1,0,1] neg_lo:[0,1,0] neg_hi:[0,1,0]
	v_pk_fma_f32 v[42:43], v[72:73], v[38:39], v[112:113] op_sel_hi:[1,0,1]
	v_pk_fma_f32 v[38:39], v[72:73], v[38:39], v[112:113] op_sel_hi:[1,0,1] neg_lo:[0,0,1] neg_hi:[0,0,1]
	v_pk_fma_f32 v[18:19], v[18:19], v[10:11], v[78:79] op_sel_hi:[1,0,1]
	v_pk_add_f32 v[78:79], v[20:21], v[82:83]
	v_pk_add_f32 v[20:21], v[20:21], v[82:83] neg_lo:[0,1] neg_hi:[0,1]
	s_nop 0
	v_pk_mul_f32 v[82:83], v[20:21], v[34:35] op_sel_hi:[1,0]
	v_xor_b32_e32 v86, 0x80000000, v21
	v_mov_b32_e32 v87, v20
	v_pk_add_f32 v[20:21], v[22:23], v[80:81]
	v_pk_add_f32 v[22:23], v[22:23], v[80:81] neg_lo:[0,1] neg_hi:[0,1]
	v_pk_mul_f32 v[72:73], v[38:39], v[122:123] op_sel:[1,0] op_sel_hi:[0,0] neg_lo:[1,1] neg_hi:[0,1]
	v_xor_b32_e32 v81, 0x80000000, v22
	v_mov_b32_e32 v80, v23
	v_pk_add_f32 v[22:23], v[26:27], v[42:43]
	v_pk_add_f32 v[26:27], v[26:27], v[42:43] neg_lo:[0,1] neg_hi:[0,1]
	v_pk_fma_f32 v[72:73], v[38:39], v[120:121], v[72:73] op_sel_hi:[1,0,1] neg_lo:[0,1,0] neg_hi:[0,1,0]
	v_pk_fma_f32 v[38:39], v[68:69], v[24:25], v[114:115] op_sel_hi:[1,0,1]
	v_pk_fma_f32 v[24:25], v[68:69], v[24:25], v[114:115] op_sel_hi:[1,0,1] neg_lo:[0,0,1] neg_hi:[0,0,1]
	v_pk_fma_f32 v[82:83], v[86:87], v[30:31], v[82:83] op_sel_hi:[1,0,1] neg_lo:[0,1,0] neg_hi:[0,1,0]
	v_pk_mul_f32 v[42:43], v[26:27], v[34:35] op_sel_hi:[1,0] neg_lo:[0,1] neg_hi:[0,1]
	s_nop 0
	v_pk_fma_f32 v[26:27], v[30:31], v[26:27], v[42:43] op_sel:[0,1,0] op_sel_hi:[0,0,1] neg_lo:[1,1,0] neg_hi:[1,0,0]
	v_pk_add_f32 v[42:43], v[28:29], v[38:39]
	v_pk_add_f32 v[28:29], v[28:29], v[38:39] neg_lo:[0,1] neg_hi:[0,1]
	v_pk_mul_f32 v[68:69], v[24:25], v[34:35] op_sel:[1,0] op_sel_hi:[0,0] neg_lo:[1,1] neg_hi:[0,1]
	v_pk_fma_f32 v[68:69], v[24:25], v[30:31], v[68:69] op_sel_hi:[1,0,1] neg_lo:[0,1,0] neg_hi:[0,1,0]
	v_pk_fma_f32 v[24:25], v[70:71], v[32:33], v[116:117] op_sel_hi:[1,0,1]
	v_pk_fma_f32 v[32:33], v[70:71], v[32:33], v[116:117] op_sel_hi:[1,0,1] neg_lo:[0,0,1] neg_hi:[0,0,1]
	v_pk_mul_f32 v[38:39], v[10:11], v[28:29] op_sel:[0,1] op_sel_hi:[0,0] neg_lo:[1,1] neg_hi:[1,0]
	v_pk_fma_f32 v[86:87], v[28:29], v[10:11], v[38:39] op_sel_hi:[1,0,1] neg_lo:[0,1,0] neg_hi:[0,1,0]
	v_pk_add_f32 v[28:29], v[44:45], v[24:25]
	v_pk_add_f32 v[24:25], v[44:45], v[24:25] neg_lo:[0,1] neg_hi:[0,1]
	v_pk_mul_f32 v[70:71], v[32:33], v[124:125] op_sel:[1,0] op_sel_hi:[0,0] neg_lo:[1,1] neg_hi:[0,1]
	v_pk_fma_f32 v[70:71], v[118:119], v[32:33], v[70:71] op_sel_hi:[0,1,1] neg_lo:[1,0,0] neg_hi:[1,0,0]
	v_pk_add_f32 v[32:33], v[126:127], v[48:49]
	v_pk_mul_f32 v[38:39], v[34:35], v[24:25] op_sel:[0,1] op_sel_hi:[0,0] neg_lo:[1,1] neg_hi:[1,0]
	v_pk_fma_f32 v[88:89], v[30:31], v[24:25], v[38:39] op_sel_hi:[0,1,1] neg_lo:[1,0,0] neg_hi:[1,0,0]
	v_pk_add_f32 v[24:25], v[32:33], v[20:21]
	v_pk_add_f32 v[32:33], v[32:33], v[20:21] neg_lo:[0,1] neg_hi:[0,1]
	v_pk_add_f32 v[20:21], v[84:85], v[22:23]
	v_pk_add_f32 v[22:23], v[84:85], v[22:23] neg_lo:[0,1] neg_hi:[0,1]
	v_pk_add_f32 v[48:49], v[126:127], v[48:49] neg_lo:[0,1] neg_hi:[0,1]
	v_pk_mul_f32 v[38:39], v[10:11], v[22:23] op_sel:[0,1] op_sel_hi:[0,0] neg_lo:[1,1] neg_hi:[1,0]
	v_pk_fma_f32 v[22:23], v[22:23], v[10:11], v[38:39] op_sel_hi:[1,0,1]
	v_pk_add_f32 v[38:39], v[16:17], v[42:43]
	v_pk_add_f32 v[16:17], v[16:17], v[42:43] neg_lo:[0,1] neg_hi:[0,1]
	s_nop 0
	v_xor_b32_e32 v43, 0x80000000, v16
	v_mov_b32_e32 v42, v17
	v_pk_add_f32 v[16:17], v[78:79], v[28:29]
	v_pk_add_f32 v[28:29], v[78:79], v[28:29] neg_lo:[0,1] neg_hi:[0,1]
	s_nop 0
	v_pk_mul_f32 v[44:45], v[10:11], v[28:29] op_sel:[0,1] op_sel_hi:[0,0] neg_lo:[1,1] neg_hi:[1,0]
	v_pk_fma_f32 v[78:79], v[10:11], v[28:29], v[44:45] op_sel_hi:[0,1,1] neg_lo:[1,0,0] neg_hi:[1,0,0]
	v_pk_add_f32 v[28:29], v[24:25], v[38:39]
	v_pk_add_f32 v[24:25], v[24:25], v[38:39] neg_lo:[0,1] neg_hi:[0,1]
	v_pk_add_f32 v[38:39], v[20:21], v[16:17]
	v_pk_add_f32 v[16:17], v[20:21], v[16:17] neg_lo:[0,1] neg_hi:[0,1]
	v_pk_add_f32 v[84:85], v[28:29], v[38:39]
	v_pk_add_f32 v[44:45], v[24:25], v[16:17] op_sel:[0,1] op_sel_hi:[1,0] neg_hi:[0,1]
	v_pk_add_f32 v[20:21], v[24:25], v[16:17] op_sel:[0,1] op_sel_hi:[1,0] neg_lo:[0,1]
	v_pk_add_f32 v[24:25], v[22:23], v[78:79]
	v_pk_add_f32 v[22:23], v[22:23], v[78:79] neg_lo:[0,1] neg_hi:[0,1]
	v_pk_add_f32 v[16:17], v[32:33], v[42:43]
	v_pk_add_f32 v[32:33], v[32:33], v[42:43] neg_lo:[0,1] neg_hi:[0,1]
	v_pk_add_f32 v[28:29], v[28:29], v[38:39] neg_lo:[0,1] neg_hi:[0,1]
	v_pk_add_f32 v[78:79], v[16:17], v[24:25]
	v_pk_add_f32 v[24:25], v[16:17], v[24:25] neg_lo:[0,1] neg_hi:[0,1]
	v_pk_add_f32 v[38:39], v[32:33], v[22:23] op_sel:[0,1] op_sel_hi:[1,0] neg_hi:[0,1]
	v_pk_add_f32 v[16:17], v[32:33], v[22:23] op_sel:[0,1] op_sel_hi:[1,0] neg_lo:[0,1]
	v_pk_add_f32 v[32:33], v[56:57], v[26:27]
	v_pk_add_f32 v[26:27], v[56:57], v[26:27] neg_lo:[0,1] neg_hi:[0,1]
	v_pk_add_f32 v[22:23], v[48:49], v[80:81]
	v_pk_add_f32 v[42:43], v[48:49], v[80:81] neg_lo:[0,1] neg_hi:[0,1]
	v_pk_mul_f32 v[48:49], v[10:11], v[26:27] op_sel:[0,1] op_sel_hi:[0,0] neg_lo:[1,1] neg_hi:[1,0]
	v_pk_fma_f32 v[26:27], v[10:11], v[26:27], v[48:49] op_sel_hi:[0,1,1]
	v_pk_add_f32 v[48:49], v[18:19], v[86:87]
	v_pk_add_f32 v[18:19], v[18:19], v[86:87] neg_lo:[0,1] neg_hi:[0,1]
	v_pk_add_f32 v[80:81], v[82:83], v[88:89] neg_lo:[0,1] neg_hi:[0,1]
	v_xor_b32_e32 v57, 0x80000000, v18
	v_mov_b32_e32 v56, v19
	v_pk_add_f32 v[18:19], v[82:83], v[88:89]
	v_pk_mul_f32 v[82:83], v[10:11], v[80:81] op_sel:[0,1] op_sel_hi:[0,0] neg_lo:[1,1] neg_hi:[1,0]
	v_pk_fma_f32 v[80:81], v[10:11], v[80:81], v[82:83] op_sel_hi:[0,1,1] neg_lo:[1,0,0] neg_hi:[1,0,0]
	v_pk_add_f32 v[82:83], v[22:23], v[48:49]
	v_pk_add_f32 v[22:23], v[22:23], v[48:49] neg_lo:[0,1] neg_hi:[0,1]
	v_pk_add_f32 v[48:49], v[32:33], v[18:19]
	v_pk_add_f32 v[18:19], v[32:33], v[18:19] neg_lo:[0,1] neg_hi:[0,1]
	v_pk_add_f32 v[88:89], v[82:83], v[48:49]
	v_xor_b32_e32 v87, 0x80000000, v18
	v_mov_b32_e32 v86, v19
	v_pk_add_f32 v[18:19], v[42:43], v[56:57]
	v_pk_add_f32 v[56:57], v[42:43], v[56:57] neg_lo:[0,1] neg_hi:[0,1]
	v_pk_add_f32 v[42:43], v[26:27], v[80:81]
	v_pk_add_f32 v[26:27], v[26:27], v[80:81] neg_lo:[0,1] neg_hi:[0,1]
	v_pk_add_f32 v[32:33], v[82:83], v[48:49] neg_lo:[0,1] neg_hi:[0,1]
	v_xor_b32_e32 v81, 0x80000000, v26
	v_mov_b32_e32 v80, v27
	v_pk_add_f32 v[82:83], v[18:19], v[42:43]
	v_pk_add_f32 v[26:27], v[18:19], v[42:43] neg_lo:[0,1] neg_hi:[0,1]
	v_pk_add_f32 v[42:43], v[56:57], v[80:81]
	v_pk_add_f32 v[18:19], v[56:57], v[80:81] neg_lo:[0,1] neg_hi:[0,1]
	v_pk_add_f32 v[56:57], v[36:37], v[76:77]
	v_pk_add_f32 v[76:77], v[36:37], v[76:77] neg_lo:[0,1] neg_hi:[0,1]
	v_pk_add_f32 v[36:37], v[40:41], v[60:61]
	v_pk_add_f32 v[40:41], v[40:41], v[60:61] neg_lo:[0,1] neg_hi:[0,1]
	v_pk_add_f32 v[48:49], v[22:23], v[86:87]
	v_pk_mul_f32 v[60:61], v[34:35], v[40:41] op_sel:[0,1] op_sel_hi:[0,0] neg_lo:[1,1] neg_hi:[1,0]
	v_pk_fma_f32 v[40:41], v[30:31], v[40:41], v[60:61] op_sel_hi:[0,1,1]
	v_pk_add_f32 v[60:61], v[46:47], v[62:63]
	v_pk_add_f32 v[46:47], v[46:47], v[62:63] neg_lo:[0,1] neg_hi:[0,1]
	v_pk_add_f32 v[22:23], v[22:23], v[86:87] neg_lo:[0,1] neg_hi:[0,1]
	v_pk_mul_f32 v[62:63], v[10:11], v[46:47] op_sel:[0,1] op_sel_hi:[0,0] neg_lo:[1,1] neg_hi:[1,0]
	v_pk_fma_f32 v[62:63], v[10:11], v[46:47], v[62:63] op_sel_hi:[0,1,1]
	v_pk_add_f32 v[46:47], v[50:51], v[58:59]
	v_pk_add_f32 v[50:51], v[50:51], v[58:59] neg_lo:[0,1] neg_hi:[0,1]
	s_nop 0
	v_pk_mul_f32 v[58:59], v[30:31], v[50:51] op_sel:[0,1] op_sel_hi:[0,0] neg_lo:[1,1] neg_hi:[1,0]
	v_pk_fma_f32 v[50:51], v[34:35], v[50:51], v[58:59] op_sel_hi:[0,1,1]
	v_pk_add_f32 v[58:59], v[52:53], v[74:75]
	v_pk_add_f32 v[52:53], v[52:53], v[74:75] neg_lo:[0,1] neg_hi:[0,1]
	s_nop 0
	v_xor_b32_e32 v75, 0x80000000, v52
	v_mov_b32_e32 v74, v53
	v_pk_add_f32 v[52:53], v[64:65], v[72:73]
	v_pk_add_f32 v[64:65], v[64:65], v[72:73] neg_lo:[0,1] neg_hi:[0,1]
	s_nop 0
	v_pk_mul_f32 v[72:73], v[30:31], v[64:65] op_sel:[0,1] op_sel_hi:[0,0] neg_lo:[1,1] neg_hi:[1,0]
	v_pk_fma_f32 v[64:65], v[34:35], v[64:65], v[72:73] op_sel_hi:[0,1,1] neg_lo:[1,0,0] neg_hi:[1,0,0]
	v_pk_add_f32 v[72:73], v[66:67], v[68:69]
	v_pk_add_f32 v[66:67], v[66:67], v[68:69] neg_lo:[0,1] neg_hi:[0,1]
	s_nop 0
	v_pk_mul_f32 v[68:69], v[10:11], v[66:67] op_sel:[0,1] op_sel_hi:[0,0] neg_lo:[1,1] neg_hi:[1,0]
	v_pk_fma_f32 v[66:67], v[10:11], v[66:67], v[68:69] op_sel_hi:[0,1,1] neg_lo:[1,0,0] neg_hi:[1,0,0]
	v_pk_add_f32 v[68:69], v[54:55], v[70:71]
	v_pk_add_f32 v[54:55], v[54:55], v[70:71] neg_lo:[0,1] neg_hi:[0,1]
	s_nop 0
	v_pk_mul_f32 v[34:35], v[34:35], v[54:55] op_sel:[0,1] op_sel_hi:[0,0] neg_lo:[1,1] neg_hi:[1,0]
	v_pk_fma_f32 v[34:35], v[30:31], v[54:55], v[34:35] op_sel_hi:[0,1,1] neg_lo:[1,0,0] neg_hi:[1,0,0]
	v_pk_add_f32 v[30:31], v[56:57], v[58:59]
	v_pk_add_f32 v[54:55], v[56:57], v[58:59] neg_lo:[0,1] neg_hi:[0,1]
	v_pk_add_f32 v[56:57], v[52:53], v[36:37]
	v_pk_add_f32 v[36:37], v[36:37], v[52:53] neg_lo:[0,1] neg_hi:[0,1]
	s_nop 0
	v_pk_mul_f32 v[52:53], v[10:11], v[36:37] op_sel:[0,1] op_sel_hi:[0,0] neg_lo:[1,1] neg_hi:[1,0]
	v_pk_fma_f32 v[58:59], v[10:11], v[36:37], v[52:53] op_sel_hi:[0,1,1]
	v_pk_add_f32 v[52:53], v[60:61], v[72:73] neg_lo:[0,1] neg_hi:[0,1]
	v_pk_add_f32 v[36:37], v[60:61], v[72:73]
	v_xor_b32_e32 v61, 0x80000000, v52
	v_mov_b32_e32 v60, v53
	v_pk_add_f32 v[52:53], v[46:47], v[68:69]
	v_pk_add_f32 v[46:47], v[46:47], v[68:69] neg_lo:[0,1] neg_hi:[0,1]
	v_pk_add_f32 v[72:73], v[64:65], v[40:41]
	v_pk_add_f32 v[40:41], v[40:41], v[64:65] neg_lo:[0,1] neg_hi:[0,1]
	v_pk_mul_f32 v[68:69], v[10:11], v[46:47] op_sel:[0,1] op_sel_hi:[0,0] neg_lo:[1,1] neg_hi:[1,0]
	v_pk_fma_f32 v[46:47], v[10:11], v[46:47], v[68:69] op_sel_hi:[0,1,1] neg_lo:[1,0,0] neg_hi:[1,0,0]
	v_pk_add_f32 v[68:69], v[30:31], v[36:37]
	v_pk_add_f32 v[30:31], v[30:31], v[36:37] neg_lo:[0,1] neg_hi:[0,1]
	v_pk_add_f32 v[36:37], v[56:57], v[52:53]
	v_pk_add_f32 v[52:53], v[56:57], v[52:53] neg_lo:[0,1] neg_hi:[0,1]
	v_pk_mul_f32 v[64:65], v[10:11], v[40:41] op_sel:[0,1] op_sel_hi:[0,0] neg_lo:[1,1] neg_hi:[1,0]
	v_xor_b32_e32 v57, 0x80000000, v52
	v_mov_b32_e32 v56, v53
	v_pk_fma_f32 v[64:65], v[10:11], v[40:41], v[64:65] op_sel_hi:[0,1,1]
	v_pk_add_f32 v[40:41], v[62:63], v[66:67]
	v_pk_add_f32 v[62:63], v[62:63], v[66:67] neg_lo:[0,1] neg_hi:[0,1]
	v_pk_add_f32 v[70:71], v[68:69], v[36:37]
	v_pk_add_f32 v[52:53], v[68:69], v[36:37] neg_lo:[0,1] neg_hi:[0,1]
	v_pk_add_f32 v[68:69], v[30:31], v[56:57]
	v_pk_add_f32 v[36:37], v[30:31], v[56:57] neg_lo:[0,1] neg_hi:[0,1]
	v_pk_add_f32 v[56:57], v[58:59], v[46:47]
	v_pk_add_f32 v[46:47], v[58:59], v[46:47] neg_lo:[0,1] neg_hi:[0,1]
	v_xor_b32_e32 v67, 0x80000000, v62
	v_mov_b32_e32 v66, v63
	v_pk_add_f32 v[62:63], v[50:51], v[34:35]
	v_pk_add_f32 v[34:35], v[50:51], v[34:35] neg_lo:[0,1] neg_hi:[0,1]
	v_pk_add_f32 v[30:31], v[54:55], v[60:61]
	v_pk_add_f32 v[54:55], v[54:55], v[60:61] neg_lo:[0,1] neg_hi:[0,1]
	v_xor_b32_e32 v59, 0x80000000, v46
	v_mov_b32_e32 v58, v47
	v_pk_add_f32 v[60:61], v[30:31], v[56:57]
	v_pk_add_f32 v[46:47], v[30:31], v[56:57] neg_lo:[0,1] neg_hi:[0,1]
	v_pk_add_f32 v[56:57], v[54:55], v[58:59]
	v_pk_add_f32 v[30:31], v[54:55], v[58:59] neg_lo:[0,1] neg_hi:[0,1]
	v_pk_add_f32 v[54:55], v[76:77], v[74:75]
	v_pk_mul_f32 v[50:51], v[10:11], v[34:35] op_sel:[0,1] op_sel_hi:[0,0] neg_lo:[1,1] neg_hi:[1,0]
	v_pk_add_f32 v[58:59], v[76:77], v[74:75] neg_lo:[0,1] neg_hi:[0,1]
	v_pk_fma_f32 v[34:35], v[10:11], v[34:35], v[50:51] op_sel_hi:[0,1,1] neg_lo:[1,0,0] neg_hi:[1,0,0]
	v_pk_add_f32 v[50:51], v[54:55], v[40:41]
	v_pk_add_f32 v[40:41], v[54:55], v[40:41] neg_lo:[0,1] neg_hi:[0,1]
	v_pk_add_f32 v[54:55], v[72:73], v[62:63]
	v_pk_add_f32 v[62:63], v[72:73], v[62:63] neg_lo:[0,1] neg_hi:[0,1]
	v_lshl_add_u32 v10, v13, 3, 0
	v_xor_b32_e32 v73, 0x80000000, v62
	v_mov_b32_e32 v72, v63
	v_pk_add_f32 v[62:63], v[50:51], v[54:55]
	v_pk_add_f32 v[54:55], v[50:51], v[54:55] neg_lo:[0,1] neg_hi:[0,1]
	v_pk_add_f32 v[50:51], v[58:59], v[66:67]
	v_pk_add_f32 v[58:59], v[58:59], v[66:67] neg_lo:[0,1] neg_hi:[0,1]
	v_pk_add_f32 v[66:67], v[64:65], v[34:35]
	v_pk_add_f32 v[34:35], v[64:65], v[34:35] neg_lo:[0,1] neg_hi:[0,1]
	v_pk_add_f32 v[74:75], v[40:41], v[72:73]
	v_pk_add_f32 v[40:41], v[40:41], v[72:73] neg_lo:[0,1] neg_hi:[0,1]
	v_pk_add_f32 v[72:73], v[50:51], v[66:67]
	v_pk_add_f32 v[50:51], v[50:51], v[66:67] neg_lo:[0,1] neg_hi:[0,1]
	v_pk_add_f32 v[66:67], v[58:59], v[34:35] op_sel:[0,1] op_sel_hi:[1,0] neg_hi:[0,1]
	v_pk_add_f32 v[34:35], v[58:59], v[34:35] op_sel:[0,1] op_sel_hi:[1,0] neg_lo:[0,1]
	v_pk_mul_f32 v[58:59], v[84:85], s[14:15] op_sel:[1,0] neg_lo:[1,0]
	s_nop 0
	v_pk_fma_f32 v[58:59], v[84:85], s[94:95], v[58:59] op_sel_hi:[0,1,1]
	ds_write_b64 v10, v[58:59]
	v_pk_fma_f32 v[58:59], v[178:179], s[90:91], v[178:179] op_sel:[1,0,0] op_sel_hi:[0,1,1]
	v_pk_mul_f32 v[64:65], v[58:59], v[70:71] op_sel:[1,1] op_sel_hi:[0,1] neg_lo:[0,1]
	v_pk_fma_f32 v[64:65], v[58:59], v[70:71], v[64:65] op_sel_hi:[1,0,1]
	ds_write_b64 v10, v[64:65] offset:4224
	v_pk_mul_f32 v[64:65], v[178:179], v[58:59] op_sel:[1,1] op_sel_hi:[0,1] neg_lo:[0,1]
	v_pk_fma_f32 v[58:59], v[178:179], v[58:59], v[64:65] op_sel_hi:[1,0,1]
	s_nop 0
	v_pk_mul_f32 v[64:65], v[58:59], v[88:89] op_sel:[1,1] op_sel_hi:[0,1] neg_lo:[0,1]
	v_pk_fma_f32 v[64:65], v[58:59], v[88:89], v[64:65] op_sel_hi:[1,0,1]
	ds_write_b64 v10, v[64:65] offset:8448
	v_pk_mul_f32 v[64:65], v[178:179], v[58:59] op_sel:[1,1] op_sel_hi:[0,1] neg_lo:[0,1]
	v_pk_fma_f32 v[58:59], v[178:179], v[58:59], v[64:65] op_sel_hi:[1,0,1]
	s_nop 0
	v_pk_mul_f32 v[64:65], v[58:59], v[62:63] op_sel:[1,1] op_sel_hi:[0,1] neg_lo:[0,1]
	v_pk_fma_f32 v[62:63], v[58:59], v[62:63], v[64:65] op_sel_hi:[1,0,1]
	ds_write_b64 v10, v[62:63] offset:12672
	v_pk_mul_f32 v[62:63], v[178:179], v[58:59] op_sel:[1,1] op_sel_hi:[0,1] neg_lo:[0,1]
	v_pk_fma_f32 v[58:59], v[178:179], v[58:59], v[62:63] op_sel_hi:[1,0,1]
	s_nop 0
	v_pk_mul_f32 v[62:63], v[58:59], v[78:79] op_sel:[1,1] op_sel_hi:[0,1] neg_lo:[0,1]
	v_pk_fma_f32 v[62:63], v[58:59], v[78:79], v[62:63] op_sel_hi:[1,0,1]
	ds_write_b64 v10, v[62:63] offset:16896
	v_pk_mul_f32 v[62:63], v[178:179], v[58:59] op_sel:[1,1] op_sel_hi:[0,1] neg_lo:[0,1]
	v_pk_fma_f32 v[58:59], v[178:179], v[58:59], v[62:63] op_sel_hi:[1,0,1]
	s_nop 0
	v_pk_mul_f32 v[62:63], v[58:59], v[60:61] op_sel:[1,1] op_sel_hi:[0,1] neg_lo:[0,1]
	v_pk_fma_f32 v[60:61], v[58:59], v[60:61], v[62:63] op_sel_hi:[1,0,1]
	ds_write_b64 v10, v[60:61] offset:21120
	v_pk_mul_f32 v[60:61], v[178:179], v[58:59] op_sel:[1,1] op_sel_hi:[0,1] neg_lo:[0,1]
	v_pk_fma_f32 v[58:59], v[178:179], v[58:59], v[60:61] op_sel_hi:[1,0,1]
	s_nop 0
	v_pk_mul_f32 v[60:61], v[82:83], v[58:59] op_sel:[1,1] op_sel_hi:[1,0] neg_lo:[1,0]
	s_nop 0
	v_pk_fma_f32 v[60:61], v[82:83], v[58:59], v[60:61] op_sel_hi:[0,1,1]
	ds_write_b64 v10, v[60:61] offset:25344
	v_pk_mul_f32 v[60:61], v[178:179], v[58:59] op_sel:[1,1] op_sel_hi:[0,1] neg_lo:[0,1]
	v_pk_fma_f32 v[58:59], v[178:179], v[58:59], v[60:61] op_sel_hi:[1,0,1]
	s_nop 0
	v_pk_mul_f32 v[60:61], v[72:73], v[58:59] op_sel:[1,1] op_sel_hi:[1,0] neg_lo:[1,0]
	s_nop 0
	v_pk_fma_f32 v[60:61], v[72:73], v[58:59], v[60:61] op_sel_hi:[0,1,1]
	ds_write_b64 v10, v[60:61] offset:29568
	v_pk_mul_f32 v[60:61], v[178:179], v[58:59] op_sel:[1,1] op_sel_hi:[0,1] neg_lo:[0,1]
	v_pk_fma_f32 v[58:59], v[178:179], v[58:59], v[60:61] op_sel_hi:[1,0,1]
	s_nop 0
	v_pk_mul_f32 v[60:61], v[44:45], v[58:59] op_sel:[1,1] op_sel_hi:[1,0] neg_lo:[1,0]
	s_nop 0
	v_pk_fma_f32 v[44:45], v[44:45], v[58:59], v[60:61] op_sel_hi:[0,1,1]
	ds_write_b64 v10, v[44:45] offset:33792
	v_pk_mul_f32 v[44:45], v[178:179], v[58:59] op_sel:[1,1] op_sel_hi:[0,1] neg_lo:[0,1]
	v_pk_fma_f32 v[44:45], v[178:179], v[58:59], v[44:45] op_sel_hi:[1,0,1]
	s_nop 0
	v_pk_mul_f32 v[58:59], v[68:69], v[44:45] op_sel:[1,1] op_sel_hi:[1,0] neg_lo:[1,0]
	s_nop 0
	v_pk_fma_f32 v[58:59], v[68:69], v[44:45], v[58:59] op_sel_hi:[0,1,1]
	ds_write_b64 v10, v[58:59] offset:38016
	v_pk_mul_f32 v[58:59], v[178:179], v[44:45] op_sel:[1,1] op_sel_hi:[0,1] neg_lo:[0,1]
	v_pk_fma_f32 v[44:45], v[178:179], v[44:45], v[58:59] op_sel_hi:[1,0,1]
	s_nop 0
	v_pk_mul_f32 v[58:59], v[48:49], v[44:45] op_sel:[1,1] op_sel_hi:[1,0] neg_lo:[1,0]
	s_nop 0
	v_pk_fma_f32 v[48:49], v[48:49], v[44:45], v[58:59] op_sel_hi:[0,1,1]
	ds_write_b64 v10, v[48:49] offset:42240
	v_pk_mul_f32 v[48:49], v[178:179], v[44:45] op_sel:[1,1] op_sel_hi:[0,1] neg_lo:[0,1]
	v_pk_fma_f32 v[44:45], v[178:179], v[44:45], v[48:49] op_sel_hi:[1,0,1]
	s_nop 0
	v_pk_mul_f32 v[48:49], v[74:75], v[44:45] op_sel:[1,1] op_sel_hi:[1,0] neg_lo:[1,0]
	s_nop 0
	v_pk_fma_f32 v[48:49], v[74:75], v[44:45], v[48:49] op_sel_hi:[0,1,1]
	ds_write_b64 v10, v[48:49] offset:46464
	v_pk_mul_f32 v[48:49], v[178:179], v[44:45] op_sel:[1,1] op_sel_hi:[0,1] neg_lo:[0,1]
	v_pk_fma_f32 v[44:45], v[178:179], v[44:45], v[48:49] op_sel_hi:[1,0,1]
	s_nop 0
	v_pk_mul_f32 v[48:49], v[38:39], v[44:45] op_sel:[1,1] op_sel_hi:[1,0] neg_lo:[1,0]
	s_nop 0
	v_pk_fma_f32 v[38:39], v[38:39], v[44:45], v[48:49] op_sel_hi:[0,1,1]
	ds_write_b64 v10, v[38:39] offset:50688
	v_pk_mul_f32 v[38:39], v[178:179], v[44:45] op_sel:[1,1] op_sel_hi:[0,1] neg_lo:[0,1]
	v_pk_fma_f32 v[38:39], v[178:179], v[44:45], v[38:39] op_sel_hi:[1,0,1]
	s_nop 0
	v_pk_mul_f32 v[44:45], v[56:57], v[38:39] op_sel:[1,1] op_sel_hi:[1,0] neg_lo:[1,0]
	s_nop 0
	v_pk_fma_f32 v[44:45], v[56:57], v[38:39], v[44:45] op_sel_hi:[0,1,1]
	ds_write_b64 v10, v[44:45] offset:54912
	v_pk_mul_f32 v[44:45], v[178:179], v[38:39] op_sel:[1,1] op_sel_hi:[0,1] neg_lo:[0,1]
	v_pk_fma_f32 v[38:39], v[178:179], v[38:39], v[44:45] op_sel_hi:[1,0,1]
	s_nop 0
	v_pk_mul_f32 v[44:45], v[42:43], v[38:39] op_sel:[1,1] op_sel_hi:[1,0] neg_lo:[1,0]
	s_nop 0
	v_pk_fma_f32 v[42:43], v[42:43], v[38:39], v[44:45] op_sel_hi:[0,1,1]
	ds_write_b64 v10, v[42:43] offset:59136
	v_pk_mul_f32 v[42:43], v[178:179], v[38:39] op_sel:[1,1] op_sel_hi:[0,1] neg_lo:[0,1]
	v_pk_fma_f32 v[38:39], v[178:179], v[38:39], v[42:43] op_sel_hi:[1,0,1]
	s_nop 0
	v_pk_mul_f32 v[42:43], v[66:67], v[38:39] op_sel:[1,1] op_sel_hi:[1,0] neg_lo:[1,0]
	s_nop 0
	v_pk_fma_f32 v[42:43], v[66:67], v[38:39], v[42:43] op_sel_hi:[0,1,1]
	ds_write_b64 v10, v[42:43] offset:63360
	v_pk_mul_f32 v[42:43], v[178:179], v[38:39] op_sel:[1,1] op_sel_hi:[0,1] neg_lo:[0,1]
	v_pk_fma_f32 v[38:39], v[178:179], v[38:39], v[42:43] op_sel_hi:[1,0,1]
	s_nop 0
	v_pk_mul_f32 v[42:43], v[28:29], v[38:39] op_sel:[1,1] op_sel_hi:[1,0] neg_lo:[1,0]
	v_add_u32_e32 v13, 0x10800, v10
	v_pk_fma_f32 v[28:29], v[28:29], v[38:39], v[42:43] op_sel_hi:[0,1,1]
	ds_write_b64 v13, v[28:29]
	v_pk_mul_f32 v[28:29], v[178:179], v[38:39] op_sel:[1,1] op_sel_hi:[0,1] neg_lo:[0,1]
	v_pk_fma_f32 v[28:29], v[178:179], v[38:39], v[28:29] op_sel_hi:[1,0,1]
	s_nop 0
	v_pk_mul_f32 v[38:39], v[52:53], v[28:29] op_sel:[1,1] op_sel_hi:[1,0] neg_lo:[1,0]
	v_add_u32_e32 v13, 0x11880, v10
	v_pk_fma_f32 v[38:39], v[52:53], v[28:29], v[38:39] op_sel_hi:[0,1,1]
	ds_write_b64 v13, v[38:39]
	v_pk_mul_f32 v[38:39], v[178:179], v[28:29] op_sel:[1,1] op_sel_hi:[0,1] neg_lo:[0,1]
	v_pk_fma_f32 v[28:29], v[178:179], v[28:29], v[38:39] op_sel_hi:[1,0,1]
	s_nop 0
	v_pk_mul_f32 v[38:39], v[32:33], v[28:29] op_sel:[1,1] op_sel_hi:[1,0] neg_lo:[1,0]
	v_add_u32_e32 v13, 0x12900, v10
	v_pk_fma_f32 v[32:33], v[32:33], v[28:29], v[38:39] op_sel_hi:[0,1,1]
	ds_write_b64 v13, v[32:33]
	v_pk_mul_f32 v[32:33], v[178:179], v[28:29] op_sel:[1,1] op_sel_hi:[0,1] neg_lo:[0,1]
	v_pk_fma_f32 v[28:29], v[178:179], v[28:29], v[32:33] op_sel_hi:[1,0,1]
	s_nop 0
	v_pk_mul_f32 v[32:33], v[54:55], v[28:29] op_sel:[1,1] op_sel_hi:[1,0] neg_lo:[1,0]
	v_add_u32_e32 v13, 0x13980, v10
	v_pk_fma_f32 v[32:33], v[54:55], v[28:29], v[32:33] op_sel_hi:[0,1,1]
	ds_write_b64 v13, v[32:33]
	v_pk_mul_f32 v[32:33], v[178:179], v[28:29] op_sel:[1,1] op_sel_hi:[0,1] neg_lo:[0,1]
	v_pk_fma_f32 v[28:29], v[178:179], v[28:29], v[32:33] op_sel_hi:[1,0,1]
	s_nop 0
	v_pk_mul_f32 v[32:33], v[24:25], v[28:29] op_sel:[1,1] op_sel_hi:[1,0] neg_lo:[1,0]
	v_add_u32_e32 v13, 0x14a00, v10
	v_pk_fma_f32 v[24:25], v[24:25], v[28:29], v[32:33] op_sel_hi:[0,1,1]
	ds_write_b64 v13, v[24:25]
	v_pk_mul_f32 v[24:25], v[178:179], v[28:29] op_sel:[1,1] op_sel_hi:[0,1] neg_lo:[0,1]
	v_pk_fma_f32 v[24:25], v[178:179], v[28:29], v[24:25] op_sel_hi:[1,0,1]
	s_nop 0
	v_pk_mul_f32 v[28:29], v[46:47], v[24:25] op_sel:[1,1] op_sel_hi:[1,0] neg_lo:[1,0]
	v_add_u32_e32 v13, 0x15a80, v10
	v_pk_fma_f32 v[28:29], v[46:47], v[24:25], v[28:29] op_sel_hi:[0,1,1]
	ds_write_b64 v13, v[28:29]
	v_pk_mul_f32 v[28:29], v[178:179], v[24:25] op_sel:[1,1] op_sel_hi:[0,1] neg_lo:[0,1]
	v_pk_fma_f32 v[24:25], v[178:179], v[24:25], v[28:29] op_sel_hi:[1,0,1]
	s_nop 0
	v_pk_mul_f32 v[28:29], v[26:27], v[24:25] op_sel:[1,1] op_sel_hi:[1,0] neg_lo:[1,0]
	v_add_u32_e32 v13, 0x16b00, v10
	v_pk_fma_f32 v[26:27], v[26:27], v[24:25], v[28:29] op_sel_hi:[0,1,1]
	ds_write_b64 v13, v[26:27]
	v_pk_mul_f32 v[26:27], v[178:179], v[24:25] op_sel:[1,1] op_sel_hi:[0,1] neg_lo:[0,1]
	v_pk_fma_f32 v[24:25], v[178:179], v[24:25], v[26:27] op_sel_hi:[1,0,1]
	s_nop 0
	v_pk_mul_f32 v[26:27], v[50:51], v[24:25] op_sel:[1,1] op_sel_hi:[1,0] neg_lo:[1,0]
	v_add_u32_e32 v13, 0x17b80, v10
	v_pk_fma_f32 v[26:27], v[50:51], v[24:25], v[26:27] op_sel_hi:[0,1,1]
	ds_write_b64 v13, v[26:27]
	v_pk_mul_f32 v[26:27], v[178:179], v[24:25] op_sel:[1,1] op_sel_hi:[0,1] neg_lo:[0,1]
	v_pk_fma_f32 v[24:25], v[178:179], v[24:25], v[26:27] op_sel_hi:[1,0,1]
	s_nop 0
	v_pk_mul_f32 v[26:27], v[20:21], v[24:25] op_sel:[1,1] op_sel_hi:[1,0] neg_lo:[1,0]
	v_add_u32_e32 v13, 0x18c00, v10
	v_pk_fma_f32 v[20:21], v[20:21], v[24:25], v[26:27] op_sel_hi:[0,1,1]
	ds_write_b64 v13, v[20:21]
	v_pk_mul_f32 v[20:21], v[178:179], v[24:25] op_sel:[1,1] op_sel_hi:[0,1] neg_lo:[0,1]
	v_pk_fma_f32 v[20:21], v[178:179], v[24:25], v[20:21] op_sel_hi:[1,0,1]
	s_nop 0
	v_pk_mul_f32 v[24:25], v[36:37], v[20:21] op_sel:[1,1] op_sel_hi:[1,0] neg_lo:[1,0]
	v_add_u32_e32 v13, 0x19c80, v10
	v_pk_fma_f32 v[24:25], v[36:37], v[20:21], v[24:25] op_sel_hi:[0,1,1]
	ds_write_b64 v13, v[24:25]
	v_pk_mul_f32 v[24:25], v[178:179], v[20:21] op_sel:[1,1] op_sel_hi:[0,1] neg_lo:[0,1]
	v_pk_fma_f32 v[20:21], v[178:179], v[20:21], v[24:25] op_sel_hi:[1,0,1]
	s_nop 0
	v_pk_mul_f32 v[24:25], v[22:23], v[20:21] op_sel:[1,1] op_sel_hi:[1,0] neg_lo:[1,0]
	v_add_u32_e32 v13, 0x1ad00, v10
	v_pk_fma_f32 v[22:23], v[22:23], v[20:21], v[24:25] op_sel_hi:[0,1,1]
	ds_write_b64 v13, v[22:23]
	v_pk_mul_f32 v[22:23], v[178:179], v[20:21] op_sel:[1,1] op_sel_hi:[0,1] neg_lo:[0,1]
	v_pk_fma_f32 v[20:21], v[178:179], v[20:21], v[22:23] op_sel_hi:[1,0,1]
	s_nop 0
	v_pk_mul_f32 v[22:23], v[40:41], v[20:21] op_sel:[1,1] op_sel_hi:[1,0] neg_lo:[1,0]
	v_add_u32_e32 v13, 0x1bd80, v10
	v_pk_fma_f32 v[22:23], v[40:41], v[20:21], v[22:23] op_sel_hi:[0,1,1]
	ds_write_b64 v13, v[22:23]
	v_pk_mul_f32 v[22:23], v[178:179], v[20:21] op_sel:[1,1] op_sel_hi:[0,1] neg_lo:[0,1]
	v_pk_fma_f32 v[20:21], v[178:179], v[20:21], v[22:23] op_sel_hi:[1,0,1]
	s_nop 0
	v_pk_mul_f32 v[22:23], v[16:17], v[20:21] op_sel:[1,1] op_sel_hi:[1,0] neg_lo:[1,0]
	v_add_u32_e32 v13, 0x1ce00, v10
	v_pk_fma_f32 v[16:17], v[16:17], v[20:21], v[22:23] op_sel_hi:[0,1,1]
	ds_write_b64 v13, v[16:17]
	v_pk_mul_f32 v[16:17], v[178:179], v[20:21] op_sel:[1,1] op_sel_hi:[0,1] neg_lo:[0,1]
	v_pk_fma_f32 v[16:17], v[178:179], v[20:21], v[16:17] op_sel_hi:[1,0,1]
	s_nop 0
	v_pk_mul_f32 v[20:21], v[30:31], v[16:17] op_sel:[1,1] op_sel_hi:[1,0] neg_lo:[1,0]
	v_add_u32_e32 v13, 0x1de80, v10
	v_pk_fma_f32 v[20:21], v[30:31], v[16:17], v[20:21] op_sel_hi:[0,1,1]
	ds_write_b64 v13, v[20:21]
	v_pk_mul_f32 v[20:21], v[178:179], v[16:17] op_sel:[1,1] op_sel_hi:[0,1] neg_lo:[0,1]
	v_pk_fma_f32 v[16:17], v[178:179], v[16:17], v[20:21] op_sel_hi:[1,0,1]
	s_nop 0
	v_pk_mul_f32 v[20:21], v[18:19], v[16:17] op_sel:[1,1] op_sel_hi:[1,0] neg_lo:[1,0]
	v_add_u32_e32 v13, 0x1ef00, v10
	v_pk_fma_f32 v[18:19], v[18:19], v[16:17], v[20:21] op_sel_hi:[0,1,1]
	ds_write_b64 v13, v[18:19]
	v_pk_mul_f32 v[18:19], v[178:179], v[16:17] op_sel:[1,1] op_sel_hi:[0,1] neg_lo:[0,1]
	v_pk_fma_f32 v[14:15], v[178:179], v[16:17], v[18:19] op_sel_hi:[1,0,1]
	s_nop 0
	v_pk_mul_f32 v[16:17], v[34:35], v[14:15] op_sel:[1,1] op_sel_hi:[1,0] neg_lo:[1,0]
	v_add_u32_e32 v10, 0x1ff80, v10
	v_pk_fma_f32 v[14:15], v[34:35], v[14:15], v[16:17] op_sel_hi:[0,1,1]
	ds_write_b64 v10, v[14:15]
	v_mov_b32_e32 v10, v174
	v_mov_b32_e32 v13, v172
	s_waitcnt lgkmcnt(0)
	s_barrier
	v_mov_b32_e32 v14, v180
	v_xad_u32 v28, v13, 3, v10
	v_lshl_add_u32 v71, v28, 3, 0
	v_xad_u32 v28, v13, 4, v10
	v_lshl_add_u32 v70, v28, 3, 0
	v_xad_u32 v28, v13, 5, v10
	v_lshl_add_u32 v69, v28, 3, 0
	v_xad_u32 v28, v13, 6, v10
	v_lshl_add_u32 v68, v28, 3, 0
	v_xad_u32 v28, v13, 7, v10
	v_lshl_add_u32 v67, v28, 3, 0
	v_xad_u32 v28, v13, 8, v10
	v_lshl_add_u32 v28, v28, 3, 0
	v_add_u32_e32 v66, 0x800, v28
	v_xad_u32 v28, v13, 9, v10
	v_lshl_add_u32 v28, v28, 3, 0
	v_add_u32_e32 v65, 0x800, v28
	v_xad_u32 v28, v13, 10, v10
	v_lshl_add_u32 v28, v28, 3, 0
	v_add_u32_e32 v64, 0x800, v28
	v_xad_u32 v28, v13, 11, v10
	v_lshl_add_u32 v28, v28, 3, 0
	v_add_u32_e32 v16, v13, v10
	v_add_u32_e32 v63, 0x800, v28
	v_xad_u32 v28, v13, 12, v10
	v_mov_b32_e32 v15, v181
	v_lshl_add_u32 v74, v16, 3, 0
	v_lshl_add_u32 v28, v28, 3, 0
	ds_read2_b64 v[16:19], v74 offset1:16
	ds_read2_b64 v[38:41], v66 offset1:16
	v_add_u32_e32 v62, 0x800, v28
	v_xad_u32 v28, v13, 13, v10
	v_xad_u32 v20, v13, 1, v10
	v_lshl_add_u32 v28, v28, 3, 0
	v_lshl_add_u32 v73, v20, 3, 0
	v_xad_u32 v24, v13, 2, v10
	v_add_u32_e32 v61, 0x800, v28
	v_xad_u32 v28, v13, 14, v10
	v_xad_u32 v10, v13, 15, v10
	ds_read2_b64 v[20:23], v73 offset0:32 offset1:48
	ds_read2_b64 v[46:49], v65 offset0:32 offset1:48
	v_lshl_add_u32 v28, v28, 3, 0
	v_lshl_add_u32 v10, v10, 3, 0
	v_lshl_add_u32 v72, v24, 3, 0
	v_add_u32_e32 v60, 0x800, v28
	v_add_u32_e32 v13, 0x800, v10
	v_mov_b32_e32 v10, v1
	ds_read2_b64 v[24:27], v72 offset0:64 offset1:80
	ds_read2_b64 v[56:59], v71 offset0:96 offset1:112
	ds_read2_b64 v[76:79], v70 offset0:128 offset1:144
	ds_read2_b64 v[80:83], v69 offset0:160 offset1:176
	ds_read2_b64 v[84:87], v68 offset0:192 offset1:208
	ds_read2_b64 v[88:91], v67 offset0:224 offset1:240
	ds_read2_b64 v[52:55], v64 offset0:64 offset1:80
	ds_read2_b64 v[92:95], v63 offset0:96 offset1:112
	ds_read2_b64 v[96:99], v62 offset0:128 offset1:144
	ds_read2_b64 v[100:103], v61 offset0:160 offset1:176
	ds_read2_b64 v[104:107], v60 offset0:192 offset1:208
	ds_read2_b64 v[108:111], v13 offset0:224 offset1:240
	s_waitcnt lgkmcnt(14)
	v_pk_add_f32 v[112:113], v[16:17], v[38:39]
	v_pk_add_f32 v[38:39], v[16:17], v[38:39] neg_lo:[0,1] neg_hi:[0,1]
	v_pk_add_f32 v[16:17], v[18:19], v[40:41]
	v_pk_add_f32 v[18:19], v[18:19], v[40:41] neg_lo:[0,1] neg_hi:[0,1]
	v_mov_b32_e32 v28, v164
	v_mov_b32_e32 v30, v165
	v_mov_b32_e32 v32, v166
	v_mov_b32_e32 v10, v167
	v_mov_b32_e32 v36, v168
	v_mov_b32_e32 v34, v169
	v_mov_b32_e32 v44, v170
	v_mov_b32_e32 v29, v171
	v_pk_mul_f32 v[40:41], v[18:19], v[44:45] op_sel:[1,0] op_sel_hi:[0,0] neg_lo:[1,1] neg_hi:[0,1]
	s_nop 0
	v_pk_fma_f32 v[42:43], v[18:19], v[28:29], v[40:41] op_sel_hi:[1,0,1]
	s_waitcnt lgkmcnt(12)
	v_pk_add_f32 v[18:19], v[20:21], v[46:47]
	v_pk_add_f32 v[20:21], v[20:21], v[46:47] neg_lo:[0,1] neg_hi:[0,1]
	s_nop 0
	v_pk_mul_f32 v[40:41], v[20:21], v[34:35] op_sel:[1,0] op_sel_hi:[0,0] neg_lo:[1,1] neg_hi:[0,1]
	s_nop 0
	v_pk_fma_f32 v[46:47], v[20:21], v[30:31], v[40:41] op_sel_hi:[1,0,1]
	v_pk_add_f32 v[20:21], v[22:23], v[48:49]
	v_pk_add_f32 v[22:23], v[22:23], v[48:49] neg_lo:[0,1] neg_hi:[0,1]
	s_nop 0
	v_pk_mul_f32 v[40:41], v[22:23], v[36:37] op_sel:[1,0] op_sel_hi:[0,0] neg_lo:[1,1] neg_hi:[0,1]
	s_nop 0
	v_pk_fma_f32 v[50:51], v[22:23], v[32:33], v[40:41] op_sel_hi:[1,0,1]
	s_waitcnt lgkmcnt(5)
	v_pk_add_f32 v[22:23], v[24:25], v[52:53]
	v_pk_add_f32 v[24:25], v[24:25], v[52:53] neg_lo:[0,1] neg_hi:[0,1]
	s_nop 0
	v_pk_mul_f32 v[40:41], v[24:25], v[10:11] op_sel:[1,0] op_sel_hi:[0,0] neg_lo:[1,1] neg_hi:[0,1]
	s_nop 0
	v_pk_fma_f32 v[52:53], v[24:25], v[10:11], v[40:41] op_sel_hi:[1,0,1]
	v_pk_add_f32 v[24:25], v[26:27], v[54:55]
	v_pk_add_f32 v[26:27], v[26:27], v[54:55] neg_lo:[0,1] neg_hi:[0,1]
	s_nop 0
	v_pk_mul_f32 v[40:41], v[26:27], v[36:37] op_sel_hi:[1,0]
	s_nop 0
	v_pk_fma_f32 v[54:55], v[26:27], v[32:33], v[40:41] op_sel:[1,0,0] op_sel_hi:[0,0,1] neg_lo:[1,1,0] neg_hi:[0,1,0]
	s_waitcnt lgkmcnt(4)
	v_pk_add_f32 v[40:41], v[56:57], v[92:93] neg_lo:[0,1] neg_hi:[0,1]
	v_pk_add_f32 v[26:27], v[56:57], v[92:93]
	v_pk_mul_f32 v[48:49], v[40:41], v[34:35] op_sel_hi:[1,0]
	s_nop 0
	v_pk_fma_f32 v[56:57], v[40:41], v[30:31], v[48:49] op_sel:[1,0,0] op_sel_hi:[0,0,1] neg_lo:[1,1,0] neg_hi:[0,1,0]
	v_pk_add_f32 v[48:49], v[58:59], v[94:95] neg_lo:[0,1] neg_hi:[0,1]
	v_pk_add_f32 v[40:41], v[58:59], v[94:95]
	v_pk_mul_f32 v[58:59], v[48:49], v[44:45] op_sel_hi:[1,0]
	v_xor_b32_e32 v92, 0x80000000, v49
	v_mov_b32_e32 v93, v48
	s_waitcnt lgkmcnt(3)
	v_pk_add_f32 v[48:49], v[76:77], v[96:97]
	v_pk_add_f32 v[76:77], v[76:77], v[96:97] neg_lo:[0,1] neg_hi:[0,1]
	v_pk_fma_f32 v[58:59], v[92:93], v[28:29], v[58:59] op_sel_hi:[1,0,1] neg_lo:[0,1,0] neg_hi:[0,1,0]
	v_xor_b32_e32 v93, 0x80000000, v76
	v_mov_b32_e32 v92, v77
	v_pk_add_f32 v[76:77], v[78:79], v[98:99]
	v_pk_add_f32 v[78:79], v[78:79], v[98:99] neg_lo:[0,1] neg_hi:[0,1]
	s_nop 0
	v_pk_mul_f32 v[94:95], v[78:79], v[44:45] op_sel_hi:[1,0] neg_lo:[0,1] neg_hi:[0,1]
	s_nop 0
	v_pk_fma_f32 v[78:79], v[78:79], v[28:29], v[94:95] op_sel:[1,0,0] op_sel_hi:[0,0,1] neg_lo:[1,1,0] neg_hi:[0,1,0]
	s_waitcnt lgkmcnt(2)
	v_pk_add_f32 v[94:95], v[80:81], v[100:101]
	v_pk_add_f32 v[80:81], v[80:81], v[100:101] neg_lo:[0,1] neg_hi:[0,1]
	s_nop 0
	v_pk_mul_f32 v[96:97], v[80:81], v[34:35] op_sel_hi:[1,0] neg_lo:[0,1] neg_hi:[0,1]
	s_nop 0
	v_pk_fma_f32 v[80:81], v[80:81], v[30:31], v[96:97] op_sel:[1,0,0] op_sel_hi:[0,0,1] neg_lo:[1,1,0] neg_hi:[0,1,0]
	v_pk_add_f32 v[96:97], v[82:83], v[102:103]
	v_pk_add_f32 v[82:83], v[82:83], v[102:103] neg_lo:[0,1] neg_hi:[0,1]
	s_nop 0
	v_pk_mul_f32 v[98:99], v[82:83], v[36:37] op_sel_hi:[1,0] neg_lo:[0,1] neg_hi:[0,1]
	s_nop 0
	v_pk_fma_f32 v[82:83], v[82:83], v[32:33], v[98:99] op_sel:[1,0,0] op_sel_hi:[0,0,1] neg_lo:[1,1,0] neg_hi:[0,1,0]
	s_waitcnt lgkmcnt(1)
	v_pk_add_f32 v[98:99], v[84:85], v[104:105]
	v_pk_add_f32 v[84:85], v[84:85], v[104:105] neg_lo:[0,1] neg_hi:[0,1]
	s_nop 0
	v_pk_mul_f32 v[100:101], v[84:85], v[10:11] op_sel:[1,0] op_sel_hi:[0,0] neg_lo:[1,1] neg_hi:[0,1]
	s_nop 0
	v_pk_fma_f32 v[84:85], v[84:85], v[10:11], v[100:101] op_sel_hi:[1,0,1] neg_lo:[0,1,0] neg_hi:[0,1,0]
	v_pk_add_f32 v[100:101], v[86:87], v[106:107]
	v_pk_add_f32 v[86:87], v[86:87], v[106:107] neg_lo:[0,1] neg_hi:[0,1]
	s_nop 0
	v_pk_mul_f32 v[36:37], v[86:87], v[36:37] op_sel:[1,0] op_sel_hi:[0,0] neg_lo:[1,1] neg_hi:[0,1]
	s_nop 0
	v_pk_fma_f32 v[86:87], v[86:87], v[32:33], v[36:37] op_sel_hi:[1,0,1] neg_lo:[0,1,0] neg_hi:[0,1,0]
	s_waitcnt lgkmcnt(0)
	v_pk_add_f32 v[36:37], v[88:89], v[108:109] neg_lo:[0,1] neg_hi:[0,1]
	v_pk_add_f32 v[32:33], v[88:89], v[108:109]
	v_pk_mul_f32 v[88:89], v[36:37], v[34:35] op_sel:[1,0] op_sel_hi:[0,0] neg_lo:[1,1] neg_hi:[0,1]
	s_nop 0
	v_pk_fma_f32 v[88:89], v[36:37], v[30:31], v[88:89] op_sel_hi:[1,0,1] neg_lo:[0,1,0] neg_hi:[0,1,0]
	v_pk_add_f32 v[36:37], v[90:91], v[110:111]
	v_pk_add_f32 v[90:91], v[90:91], v[110:111] neg_lo:[0,1] neg_hi:[0,1]
	s_nop 0
	v_pk_mul_f32 v[44:45], v[90:91], v[44:45] op_sel:[1,0] op_sel_hi:[0,0] neg_lo:[1,1] neg_hi:[0,1]
	s_nop 0
	v_pk_fma_f32 v[90:91], v[90:91], v[28:29], v[44:45] op_sel_hi:[1,0,1] neg_lo:[0,1,0] neg_hi:[0,1,0]
	v_pk_add_f32 v[44:45], v[16:17], v[76:77]
	v_pk_add_f32 v[16:17], v[16:17], v[76:77] neg_lo:[0,1] neg_hi:[0,1]
	v_pk_add_f32 v[28:29], v[112:113], v[48:49]
	v_pk_mul_f32 v[76:77], v[16:17], v[34:35] op_sel:[1,0] op_sel_hi:[0,0] neg_lo:[1,1] neg_hi:[0,1]
	v_pk_add_f32 v[48:49], v[112:113], v[48:49] neg_lo:[0,1] neg_hi:[0,1]
	v_pk_fma_f32 v[76:77], v[16:17], v[30:31], v[76:77] op_sel_hi:[1,0,1]
	v_pk_add_f32 v[16:17], v[18:19], v[94:95]
	v_pk_add_f32 v[18:19], v[18:19], v[94:95] neg_lo:[0,1] neg_hi:[0,1]
	s_nop 0
	v_pk_mul_f32 v[94:95], v[18:19], v[10:11] op_sel:[1,0] op_sel_hi:[0,0] neg_lo:[1,1] neg_hi:[0,1]
	s_nop 0
	v_pk_fma_f32 v[18:19], v[18:19], v[10:11], v[94:95] op_sel_hi:[1,0,1]
	v_pk_add_f32 v[94:95], v[20:21], v[96:97]
	v_pk_add_f32 v[20:21], v[20:21], v[96:97] neg_lo:[0,1] neg_hi:[0,1]
	s_nop 0
	v_pk_mul_f32 v[96:97], v[20:21], v[34:35] op_sel_hi:[1,0]
	v_xor_b32_e32 v102, 0x80000000, v21
	v_mov_b32_e32 v103, v20
	v_pk_add_f32 v[20:21], v[22:23], v[98:99]
	v_pk_add_f32 v[22:23], v[22:23], v[98:99] neg_lo:[0,1] neg_hi:[0,1]
	v_pk_fma_f32 v[96:97], v[102:103], v[30:31], v[96:97] op_sel_hi:[1,0,1] neg_lo:[0,1,0] neg_hi:[0,1,0]
	v_xor_b32_e32 v99, 0x80000000, v22
	v_mov_b32_e32 v98, v23
	v_pk_add_f32 v[22:23], v[24:25], v[100:101]
	v_pk_add_f32 v[24:25], v[24:25], v[100:101] neg_lo:[0,1] neg_hi:[0,1]
	s_nop 0
	v_pk_mul_f32 v[100:101], v[24:25], v[34:35] op_sel_hi:[1,0] neg_lo:[0,1] neg_hi:[0,1]
	v_xor_b32_e32 v102, 0x80000000, v25
	v_mov_b32_e32 v103, v24
	v_pk_add_f32 v[24:25], v[26:27], v[32:33]
	v_pk_add_f32 v[26:27], v[26:27], v[32:33] neg_lo:[0,1] neg_hi:[0,1]
	v_pk_fma_f32 v[100:101], v[102:103], v[30:31], v[100:101] op_sel_hi:[1,0,1] neg_lo:[0,1,0] neg_hi:[0,1,0]
	v_pk_mul_f32 v[32:33], v[26:27], v[10:11] op_sel:[1,0] op_sel_hi:[0,0] neg_lo:[1,1] neg_hi:[0,1]
	v_pk_add_f32 v[102:103], v[28:29], v[20:21] neg_lo:[0,1] neg_hi:[0,1]
	v_pk_fma_f32 v[26:27], v[26:27], v[10:11], v[32:33] op_sel_hi:[1,0,1] neg_lo:[0,1,0] neg_hi:[0,1,0]
	v_pk_add_f32 v[32:33], v[40:41], v[36:37]
	v_pk_add_f32 v[36:37], v[40:41], v[36:37] neg_lo:[0,1] neg_hi:[0,1]
	s_nop 0
	v_pk_mul_f32 v[40:41], v[36:37], v[34:35] op_sel:[1,0] op_sel_hi:[0,0] neg_lo:[1,1] neg_hi:[0,1]
	s_nop 0
	v_pk_fma_f32 v[40:41], v[36:37], v[30:31], v[40:41] op_sel_hi:[1,0,1] neg_lo:[0,1,0] neg_hi:[0,1,0]
	v_pk_add_f32 v[36:37], v[28:29], v[20:21]
	v_pk_add_f32 v[20:21], v[44:45], v[22:23]
	v_pk_add_f32 v[22:23], v[44:45], v[22:23] neg_lo:[0,1] neg_hi:[0,1]
	s_nop 0
	v_pk_mul_f32 v[28:29], v[22:23], v[10:11] op_sel:[1,0] op_sel_hi:[0,0] neg_lo:[1,1] neg_hi:[0,1]
	s_nop 0
	v_pk_fma_f32 v[22:23], v[22:23], v[10:11], v[28:29] op_sel_hi:[1,0,1]
	v_pk_add_f32 v[28:29], v[16:17], v[24:25]
	v_pk_add_f32 v[16:17], v[16:17], v[24:25] neg_lo:[0,1] neg_hi:[0,1]
	s_nop 0
	v_xor_b32_e32 v25, 0x80000000, v16
	v_mov_b32_e32 v24, v17
	v_pk_add_f32 v[16:17], v[94:95], v[32:33]
	v_pk_add_f32 v[32:33], v[94:95], v[32:33] neg_lo:[0,1] neg_hi:[0,1]
	s_nop 0
	v_pk_mul_f32 v[44:45], v[32:33], v[10:11] op_sel:[1,0] op_sel_hi:[0,0] neg_lo:[1,1] neg_hi:[0,1]
	s_nop 0
	v_pk_fma_f32 v[32:33], v[32:33], v[10:11], v[44:45] op_sel_hi:[1,0,1] neg_lo:[0,1,0] neg_hi:[0,1,0]
	v_pk_add_f32 v[44:45], v[36:37], v[28:29]
	v_pk_add_f32 v[36:37], v[36:37], v[28:29] neg_lo:[0,1] neg_hi:[0,1]
	v_pk_add_f32 v[28:29], v[20:21], v[16:17]
	v_pk_add_f32 v[16:17], v[20:21], v[16:17] neg_lo:[0,1] neg_hi:[0,1]
	v_pk_add_f32 v[94:95], v[44:45], v[28:29]
	v_xor_b32_e32 v21, 0x80000000, v16
	v_mov_b32_e32 v20, v17
	v_pk_add_f32 v[16:17], v[102:103], v[24:25]
	v_pk_add_f32 v[102:103], v[102:103], v[24:25] neg_lo:[0,1] neg_hi:[0,1]
	v_pk_add_f32 v[24:25], v[22:23], v[32:33]
	v_pk_add_f32 v[22:23], v[22:23], v[32:33] neg_lo:[0,1] neg_hi:[0,1]
	v_pk_add_f32 v[28:29], v[44:45], v[28:29] neg_lo:[0,1] neg_hi:[0,1]
	v_xor_b32_e32 v33, 0x80000000, v22
	v_mov_b32_e32 v32, v23
	v_pk_add_f32 v[22:23], v[48:49], v[98:99]
	v_pk_add_f32 v[98:99], v[48:49], v[98:99] neg_lo:[0,1] neg_hi:[0,1]
	v_pk_add_f32 v[48:49], v[76:77], v[100:101] neg_lo:[0,1] neg_hi:[0,1]
	v_pk_add_f32 v[44:45], v[36:37], v[20:21]
	v_pk_add_f32 v[20:21], v[36:37], v[20:21] neg_lo:[0,1] neg_hi:[0,1]
	v_pk_add_f32 v[104:105], v[16:17], v[24:25]
	v_pk_add_f32 v[24:25], v[16:17], v[24:25] neg_lo:[0,1] neg_hi:[0,1]
	v_pk_add_f32 v[36:37], v[102:103], v[32:33]
	v_pk_add_f32 v[16:17], v[102:103], v[32:33] neg_lo:[0,1] neg_hi:[0,1]
	v_pk_add_f32 v[32:33], v[76:77], v[100:101]
	v_pk_mul_f32 v[76:77], v[10:11], v[48:49] op_sel:[0,1] op_sel_hi:[0,0] neg_lo:[1,1] neg_hi:[1,0]
	v_pk_fma_f32 v[76:77], v[10:11], v[48:49], v[76:77] op_sel_hi:[0,1,1]
	v_pk_add_f32 v[48:49], v[18:19], v[26:27]
	v_pk_add_f32 v[18:19], v[18:19], v[26:27] neg_lo:[0,1] neg_hi:[0,1]
	s_nop 0
	v_xor_b32_e32 v27, 0x80000000, v18
	v_mov_b32_e32 v26, v19
	v_pk_add_f32 v[18:19], v[96:97], v[40:41]
	v_pk_add_f32 v[40:41], v[96:97], v[40:41] neg_lo:[0,1] neg_hi:[0,1]
	s_nop 0
	v_pk_mul_f32 v[96:97], v[10:11], v[40:41] op_sel:[0,1] op_sel_hi:[0,0] neg_lo:[1,1] neg_hi:[1,0]
	v_pk_fma_f32 v[40:41], v[10:11], v[40:41], v[96:97] op_sel_hi:[0,1,1] neg_lo:[1,0,0] neg_hi:[1,0,0]
	v_pk_add_f32 v[96:97], v[22:23], v[48:49]
	v_pk_add_f32 v[22:23], v[22:23], v[48:49] neg_lo:[0,1] neg_hi:[0,1]
	v_pk_add_f32 v[48:49], v[32:33], v[18:19]
	v_pk_add_f32 v[18:19], v[32:33], v[18:19] neg_lo:[0,1] neg_hi:[0,1]
	v_pk_add_f32 v[102:103], v[96:97], v[48:49]
	v_xor_b32_e32 v101, 0x80000000, v18
	v_mov_b32_e32 v100, v19
	v_pk_add_f32 v[32:33], v[96:97], v[48:49] neg_lo:[0,1] neg_hi:[0,1]
	v_pk_add_f32 v[18:19], v[98:99], v[26:27]
	v_pk_add_f32 v[96:97], v[98:99], v[26:27] neg_lo:[0,1] neg_hi:[0,1]
	v_pk_add_f32 v[26:27], v[76:77], v[40:41]
	v_pk_add_f32 v[40:41], v[76:77], v[40:41] neg_lo:[0,1] neg_hi:[0,1]
	v_pk_add_f32 v[98:99], v[18:19], v[26:27]
	v_xor_b32_e32 v77, 0x80000000, v40
	v_mov_b32_e32 v76, v41
	v_pk_add_f32 v[26:27], v[18:19], v[26:27] neg_lo:[0,1] neg_hi:[0,1]
	v_pk_add_f32 v[40:41], v[96:97], v[76:77]
	v_pk_add_f32 v[18:19], v[96:97], v[76:77] neg_lo:[0,1] neg_hi:[0,1]
	v_pk_add_f32 v[76:77], v[38:39], v[92:93]
	v_pk_add_f32 v[92:93], v[38:39], v[92:93] neg_lo:[0,1] neg_hi:[0,1]
	v_pk_add_f32 v[38:39], v[42:43], v[78:79]
	v_pk_add_f32 v[42:43], v[42:43], v[78:79] neg_lo:[0,1] neg_hi:[0,1]
	v_pk_add_f32 v[48:49], v[22:23], v[100:101]
	v_pk_mul_f32 v[78:79], v[34:35], v[42:43] op_sel:[0,1] op_sel_hi:[0,0] neg_lo:[1,1] neg_hi:[1,0]
	v_pk_fma_f32 v[42:43], v[30:31], v[42:43], v[78:79] op_sel_hi:[0,1,1]
	v_pk_add_f32 v[78:79], v[46:47], v[80:81]
	v_pk_add_f32 v[46:47], v[46:47], v[80:81] neg_lo:[0,1] neg_hi:[0,1]
	v_pk_add_f32 v[22:23], v[22:23], v[100:101] neg_lo:[0,1] neg_hi:[0,1]
	v_pk_mul_f32 v[80:81], v[10:11], v[46:47] op_sel:[0,1] op_sel_hi:[0,0] neg_lo:[1,1] neg_hi:[1,0]
	v_pk_fma_f32 v[80:81], v[10:11], v[46:47], v[80:81] op_sel_hi:[0,1,1]
	v_pk_add_f32 v[46:47], v[50:51], v[82:83]
	v_pk_add_f32 v[50:51], v[50:51], v[82:83] neg_lo:[0,1] neg_hi:[0,1]
	s_nop 0
	v_pk_mul_f32 v[82:83], v[30:31], v[50:51] op_sel:[0,1] op_sel_hi:[0,0] neg_lo:[1,1] neg_hi:[1,0]
	v_pk_fma_f32 v[50:51], v[34:35], v[50:51], v[82:83] op_sel_hi:[0,1,1]
	v_pk_add_f32 v[82:83], v[52:53], v[84:85]
	v_pk_add_f32 v[52:53], v[52:53], v[84:85] neg_lo:[0,1] neg_hi:[0,1]
	s_nop 0
	v_xor_b32_e32 v85, 0x80000000, v52
	v_mov_b32_e32 v84, v53
	v_pk_add_f32 v[52:53], v[54:55], v[86:87]
	v_pk_add_f32 v[54:55], v[54:55], v[86:87] neg_lo:[0,1] neg_hi:[0,1]
	s_nop 0
	v_pk_mul_f32 v[86:87], v[30:31], v[54:55] op_sel:[0,1] op_sel_hi:[0,0] neg_lo:[1,1] neg_hi:[1,0]
	v_pk_fma_f32 v[54:55], v[34:35], v[54:55], v[86:87] op_sel_hi:[0,1,1] neg_lo:[1,0,0] neg_hi:[1,0,0]
	v_pk_add_f32 v[86:87], v[56:57], v[88:89]
	v_pk_add_f32 v[56:57], v[56:57], v[88:89] neg_lo:[0,1] neg_hi:[0,1]
	s_nop 0
	v_pk_mul_f32 v[88:89], v[10:11], v[56:57] op_sel:[0,1] op_sel_hi:[0,0] neg_lo:[1,1] neg_hi:[1,0]
	v_pk_fma_f32 v[56:57], v[10:11], v[56:57], v[88:89] op_sel_hi:[0,1,1] neg_lo:[1,0,0] neg_hi:[1,0,0]
	v_pk_add_f32 v[88:89], v[58:59], v[90:91]
	v_pk_add_f32 v[58:59], v[58:59], v[90:91] neg_lo:[0,1] neg_hi:[0,1]
	s_nop 0
	v_pk_mul_f32 v[34:35], v[34:35], v[58:59] op_sel:[0,1] op_sel_hi:[0,0] neg_lo:[1,1] neg_hi:[1,0]
	v_pk_fma_f32 v[34:35], v[30:31], v[58:59], v[34:35] op_sel_hi:[0,1,1] neg_lo:[1,0,0] neg_hi:[1,0,0]
	v_pk_add_f32 v[30:31], v[76:77], v[82:83]
	v_pk_add_f32 v[58:59], v[76:77], v[82:83] neg_lo:[0,1] neg_hi:[0,1]
	v_pk_add_f32 v[76:77], v[52:53], v[38:39]
	v_pk_add_f32 v[38:39], v[38:39], v[52:53] neg_lo:[0,1] neg_hi:[0,1]
	s_nop 0
	v_pk_mul_f32 v[52:53], v[10:11], v[38:39] op_sel:[0,1] op_sel_hi:[0,0] neg_lo:[1,1] neg_hi:[1,0]
	v_pk_fma_f32 v[52:53], v[10:11], v[38:39], v[52:53] op_sel_hi:[0,1,1]
	v_pk_add_f32 v[38:39], v[78:79], v[86:87]
	v_pk_add_f32 v[78:79], v[78:79], v[86:87] neg_lo:[0,1] neg_hi:[0,1]
	s_nop 0
	v_xor_b32_e32 v83, 0x80000000, v78
	v_mov_b32_e32 v82, v79
	v_pk_add_f32 v[78:79], v[46:47], v[88:89]
	v_pk_add_f32 v[46:47], v[46:47], v[88:89] neg_lo:[0,1] neg_hi:[0,1]
	v_pk_add_f32 v[88:89], v[76:77], v[78:79]
	v_pk_mul_f32 v[86:87], v[10:11], v[46:47] op_sel:[0,1] op_sel_hi:[0,0] neg_lo:[1,1] neg_hi:[1,0]
	v_pk_fma_f32 v[46:47], v[10:11], v[46:47], v[86:87] op_sel_hi:[0,1,1] neg_lo:[1,0,0] neg_hi:[1,0,0]
	v_pk_add_f32 v[86:87], v[30:31], v[38:39]
	v_pk_add_f32 v[30:31], v[30:31], v[38:39] neg_lo:[0,1] neg_hi:[0,1]
	v_pk_add_f32 v[38:39], v[76:77], v[78:79] neg_lo:[0,1] neg_hi:[0,1]
	v_pk_add_f32 v[78:79], v[86:87], v[88:89] neg_lo:[0,1] neg_hi:[0,1]
	v_pk_add_f32 v[90:91], v[30:31], v[38:39] op_sel:[0,1] op_sel_hi:[1,0] neg_hi:[0,1]
	v_pk_add_f32 v[38:39], v[30:31], v[38:39] op_sel:[0,1] op_sel_hi:[1,0] neg_lo:[0,1]
	v_pk_add_f32 v[76:77], v[52:53], v[46:47]
	v_pk_add_f32 v[46:47], v[52:53], v[46:47] neg_lo:[0,1] neg_hi:[0,1]
	v_pk_add_f32 v[30:31], v[58:59], v[82:83]
	v_pk_add_f32 v[58:59], v[58:59], v[82:83] neg_lo:[0,1] neg_hi:[0,1]
	v_xor_b32_e32 v53, 0x80000000, v46
	v_mov_b32_e32 v52, v47
	v_pk_add_f32 v[82:83], v[30:31], v[76:77]
	v_pk_add_f32 v[46:47], v[30:31], v[76:77] neg_lo:[0,1] neg_hi:[0,1]
	v_pk_add_f32 v[76:77], v[58:59], v[52:53]
	v_pk_add_f32 v[30:31], v[58:59], v[52:53] neg_lo:[0,1] neg_hi:[0,1]
	v_pk_add_f32 v[52:53], v[92:93], v[84:85]
	v_pk_add_f32 v[58:59], v[92:93], v[84:85] neg_lo:[0,1] neg_hi:[0,1]
	v_pk_add_f32 v[84:85], v[54:55], v[42:43]
	v_pk_add_f32 v[42:43], v[42:43], v[54:55] neg_lo:[0,1] neg_hi:[0,1]
	v_pk_add_f32 v[86:87], v[86:87], v[88:89]
	v_pk_mul_f32 v[54:55], v[10:11], v[42:43] op_sel:[0,1] op_sel_hi:[0,0] neg_lo:[1,1] neg_hi:[1,0]
	v_pk_fma_f32 v[54:55], v[10:11], v[42:43], v[54:55] op_sel_hi:[0,1,1]
	v_pk_add_f32 v[42:43], v[80:81], v[56:57]
	v_pk_add_f32 v[56:57], v[80:81], v[56:57] neg_lo:[0,1] neg_hi:[0,1]
	s_nop 0
	v_xor_b32_e32 v81, 0x80000000, v56
	v_mov_b32_e32 v80, v57
	v_pk_add_f32 v[56:57], v[50:51], v[34:35]
	v_pk_add_f32 v[34:35], v[50:51], v[34:35] neg_lo:[0,1] neg_hi:[0,1]
	s_nop 0
	v_pk_mul_f32 v[50:51], v[10:11], v[34:35] op_sel:[0,1] op_sel_hi:[0,0] neg_lo:[1,1] neg_hi:[1,0]
	v_pk_fma_f32 v[34:35], v[10:11], v[34:35], v[50:51] op_sel_hi:[0,1,1] neg_lo:[1,0,0] neg_hi:[1,0,0]
	v_pk_add_f32 v[50:51], v[52:53], v[42:43]
	v_pk_add_f32 v[42:43], v[52:53], v[42:43] neg_lo:[0,1] neg_hi:[0,1]
	v_pk_add_f32 v[52:53], v[84:85], v[56:57]
	v_pk_add_f32 v[56:57], v[84:85], v[56:57] neg_lo:[0,1] neg_hi:[0,1]
	s_nop 0
	v_xor_b32_e32 v85, 0x80000000, v56
	v_mov_b32_e32 v84, v57
	v_pk_add_f32 v[56:57], v[50:51], v[52:53]
	v_pk_add_f32 v[50:51], v[50:51], v[52:53] neg_lo:[0,1] neg_hi:[0,1]
	v_pk_add_f32 v[52:53], v[42:43], v[84:85]
	v_pk_add_f32 v[42:43], v[42:43], v[84:85] neg_lo:[0,1] neg_hi:[0,1]
	v_pk_add_f32 v[84:85], v[58:59], v[80:81]
	v_pk_add_f32 v[58:59], v[58:59], v[80:81] neg_lo:[0,1] neg_hi:[0,1]
	v_pk_add_f32 v[80:81], v[54:55], v[34:35]
	v_pk_add_f32 v[34:35], v[54:55], v[34:35] neg_lo:[0,1] neg_hi:[0,1]
	v_pk_add_f32 v[92:93], v[84:85], v[80:81]
	v_pk_add_f32 v[80:81], v[84:85], v[80:81] neg_lo:[0,1] neg_hi:[0,1]
	v_pk_add_f32 v[84:85], v[58:59], v[34:35] op_sel:[0,1] op_sel_hi:[1,0] neg_hi:[0,1]
	v_pk_add_f32 v[34:35], v[58:59], v[34:35] op_sel:[0,1] op_sel_hi:[1,0] neg_lo:[0,1]
	v_pk_fma_f32 v[58:59], v[14:15], s[90:91], v[14:15] op_sel:[1,0,0] op_sel_hi:[0,1,1]
	v_pk_mul_f32 v[54:55], v[94:95], s[14:15] op_sel:[1,0] neg_lo:[1,0]
	v_pk_mul_f32 v[88:89], v[58:59], v[86:87] op_sel:[1,1] op_sel_hi:[0,1] neg_lo:[0,1]
	v_pk_fma_f32 v[54:55], v[94:95], s[94:95], v[54:55] op_sel_hi:[0,1,1]
	v_pk_fma_f32 v[86:87], v[58:59], v[86:87], v[88:89] op_sel_hi:[1,0,1]
	ds_write2_b64 v74, v[54:55], v[86:87] offset1:16
	v_pk_mul_f32 v[54:55], v[14:15], v[58:59] op_sel:[1,1] op_sel_hi:[0,1] neg_lo:[0,1]
	v_pk_fma_f32 v[54:55], v[14:15], v[58:59], v[54:55] op_sel_hi:[1,0,1]
	s_nop 0
	v_pk_mul_f32 v[58:59], v[54:55], v[102:103] op_sel:[1,1] op_sel_hi:[0,1] neg_lo:[0,1]
	v_pk_mul_f32 v[74:75], v[14:15], v[54:55] op_sel:[1,1] op_sel_hi:[0,1] neg_lo:[0,1]
	v_pk_fma_f32 v[58:59], v[54:55], v[102:103], v[58:59] op_sel_hi:[1,0,1]
	v_pk_fma_f32 v[54:55], v[14:15], v[54:55], v[74:75] op_sel_hi:[1,0,1]
	s_nop 0
	v_pk_mul_f32 v[74:75], v[54:55], v[56:57] op_sel:[1,1] op_sel_hi:[0,1] neg_lo:[0,1]
	v_pk_fma_f32 v[56:57], v[54:55], v[56:57], v[74:75] op_sel_hi:[1,0,1]
	ds_write2_b64 v73, v[58:59], v[56:57] offset0:32 offset1:48
	v_pk_mul_f32 v[56:57], v[14:15], v[54:55] op_sel:[1,1] op_sel_hi:[0,1] neg_lo:[0,1]
	v_pk_fma_f32 v[54:55], v[14:15], v[54:55], v[56:57] op_sel_hi:[1,0,1]
	s_nop 0
	v_pk_mul_f32 v[56:57], v[54:55], v[104:105] op_sel:[1,1] op_sel_hi:[0,1] neg_lo:[0,1]
	v_pk_mul_f32 v[58:59], v[14:15], v[54:55] op_sel:[1,1] op_sel_hi:[0,1] neg_lo:[0,1]
	v_pk_fma_f32 v[56:57], v[54:55], v[104:105], v[56:57] op_sel_hi:[1,0,1]
	v_pk_fma_f32 v[54:55], v[14:15], v[54:55], v[58:59] op_sel_hi:[1,0,1]
	s_nop 0
	v_pk_mul_f32 v[58:59], v[54:55], v[82:83] op_sel:[1,1] op_sel_hi:[0,1] neg_lo:[0,1]
	v_pk_fma_f32 v[58:59], v[54:55], v[82:83], v[58:59] op_sel_hi:[1,0,1]
	ds_write2_b64 v72, v[56:57], v[58:59] offset0:64 offset1:80
	v_pk_mul_f32 v[56:57], v[14:15], v[54:55] op_sel:[1,1] op_sel_hi:[0,1] neg_lo:[0,1]
	v_pk_fma_f32 v[54:55], v[14:15], v[54:55], v[56:57] op_sel_hi:[1,0,1]
	s_nop 0
	v_pk_mul_f32 v[56:57], v[54:55], v[98:99] op_sel:[1,1] op_sel_hi:[0,1] neg_lo:[0,1]
	v_pk_mul_f32 v[58:59], v[14:15], v[54:55] op_sel:[1,1] op_sel_hi:[0,1] neg_lo:[0,1]
	v_pk_fma_f32 v[56:57], v[54:55], v[98:99], v[56:57] op_sel_hi:[1,0,1]
	v_pk_fma_f32 v[54:55], v[14:15], v[54:55], v[58:59] op_sel_hi:[1,0,1]
	s_nop 0
	v_pk_mul_f32 v[58:59], v[54:55], v[92:93] op_sel:[1,1] op_sel_hi:[0,1] neg_lo:[0,1]
	v_pk_fma_f32 v[58:59], v[54:55], v[92:93], v[58:59] op_sel_hi:[1,0,1]
	ds_write2_b64 v71, v[56:57], v[58:59] offset0:96 offset1:112
	v_pk_mul_f32 v[56:57], v[14:15], v[54:55] op_sel:[1,1] op_sel_hi:[0,1] neg_lo:[0,1]
	v_pk_fma_f32 v[54:55], v[14:15], v[54:55], v[56:57] op_sel_hi:[1,0,1]
	s_nop 0
	v_pk_mul_f32 v[56:57], v[54:55], v[44:45] op_sel:[1,1] op_sel_hi:[0,1] neg_lo:[0,1]
	v_pk_fma_f32 v[44:45], v[54:55], v[44:45], v[56:57] op_sel_hi:[1,0,1]
	v_pk_mul_f32 v[56:57], v[14:15], v[54:55] op_sel:[1,1] op_sel_hi:[0,1] neg_lo:[0,1]
	v_pk_fma_f32 v[54:55], v[14:15], v[54:55], v[56:57] op_sel_hi:[1,0,1]
	s_nop 0
	v_pk_mul_f32 v[56:57], v[54:55], v[90:91] op_sel:[1,1] op_sel_hi:[0,1] neg_lo:[0,1]
	v_pk_fma_f32 v[56:57], v[54:55], v[90:91], v[56:57] op_sel_hi:[1,0,1]
	ds_write2_b64 v70, v[44:45], v[56:57] offset0:128 offset1:144
	v_pk_mul_f32 v[44:45], v[14:15], v[54:55] op_sel:[1,1] op_sel_hi:[0,1] neg_lo:[0,1]
	v_pk_fma_f32 v[44:45], v[14:15], v[54:55], v[44:45] op_sel_hi:[1,0,1]
	s_nop 0
	v_pk_mul_f32 v[54:55], v[44:45], v[48:49] op_sel:[1,1] op_sel_hi:[0,1] neg_lo:[0,1]
	v_pk_fma_f32 v[48:49], v[44:45], v[48:49], v[54:55] op_sel_hi:[1,0,1]
	v_pk_mul_f32 v[54:55], v[14:15], v[44:45] op_sel:[1,1] op_sel_hi:[0,1] neg_lo:[0,1]
	v_pk_fma_f32 v[44:45], v[14:15], v[44:45], v[54:55] op_sel_hi:[1,0,1]
	s_nop 0
	v_pk_mul_f32 v[54:55], v[44:45], v[52:53] op_sel:[1,1] op_sel_hi:[0,1] neg_lo:[0,1]
	v_pk_fma_f32 v[52:53], v[44:45], v[52:53], v[54:55] op_sel_hi:[1,0,1]
	ds_write2_b64 v69, v[48:49], v[52:53] offset0:160 offset1:176
	v_pk_mul_f32 v[48:49], v[14:15], v[44:45] op_sel:[1,1] op_sel_hi:[0,1] neg_lo:[0,1]
	v_pk_fma_f32 v[44:45], v[14:15], v[44:45], v[48:49] op_sel_hi:[1,0,1]
	s_nop 0
	v_pk_mul_f32 v[48:49], v[36:37], v[44:45] op_sel:[1,1] op_sel_hi:[1,0] neg_lo:[1,0]
	s_nop 0
	v_pk_fma_f32 v[36:37], v[36:37], v[44:45], v[48:49] op_sel_hi:[0,1,1]
	v_pk_mul_f32 v[48:49], v[14:15], v[44:45] op_sel:[1,1] op_sel_hi:[0,1] neg_lo:[0,1]
	v_pk_fma_f32 v[44:45], v[14:15], v[44:45], v[48:49] op_sel_hi:[1,0,1]
	s_nop 0
	v_pk_mul_f32 v[48:49], v[44:45], v[76:77] op_sel:[1,1] op_sel_hi:[0,1] neg_lo:[0,1]
	v_pk_fma_f32 v[48:49], v[44:45], v[76:77], v[48:49] op_sel_hi:[1,0,1]
	ds_write2_b64 v68, v[36:37], v[48:49] offset0:192 offset1:208
	v_pk_mul_f32 v[36:37], v[14:15], v[44:45] op_sel:[1,1] op_sel_hi:[0,1] neg_lo:[0,1]
	v_pk_fma_f32 v[36:37], v[14:15], v[44:45], v[36:37] op_sel_hi:[1,0,1]
	s_nop 0
	v_pk_mul_f32 v[44:45], v[40:41], v[36:37] op_sel:[1,1] op_sel_hi:[1,0] neg_lo:[1,0]
	s_nop 0
	v_pk_fma_f32 v[40:41], v[40:41], v[36:37], v[44:45] op_sel_hi:[0,1,1]
	v_pk_mul_f32 v[44:45], v[14:15], v[36:37] op_sel:[1,1] op_sel_hi:[0,1] neg_lo:[0,1]
	v_pk_fma_f32 v[36:37], v[14:15], v[36:37], v[44:45] op_sel_hi:[1,0,1]
	s_nop 0
	v_pk_mul_f32 v[44:45], v[36:37], v[84:85] op_sel:[1,1] op_sel_hi:[0,1] neg_lo:[0,1]
	v_pk_fma_f32 v[44:45], v[36:37], v[84:85], v[44:45] op_sel_hi:[1,0,1]
	ds_write2_b64 v67, v[40:41], v[44:45] offset0:224 offset1:240
	v_pk_mul_f32 v[40:41], v[14:15], v[36:37] op_sel:[1,1] op_sel_hi:[0,1] neg_lo:[0,1]
	v_pk_fma_f32 v[36:37], v[14:15], v[36:37], v[40:41] op_sel_hi:[1,0,1]
	s_nop 0
	v_pk_mul_f32 v[40:41], v[28:29], v[36:37] op_sel:[1,1] op_sel_hi:[1,0] neg_lo:[1,0]
	s_nop 0
	v_pk_fma_f32 v[28:29], v[28:29], v[36:37], v[40:41] op_sel_hi:[0,1,1]
	v_pk_mul_f32 v[40:41], v[14:15], v[36:37] op_sel:[1,1] op_sel_hi:[0,1] neg_lo:[0,1]
	v_pk_fma_f32 v[36:37], v[14:15], v[36:37], v[40:41] op_sel_hi:[1,0,1]
	s_nop 0
	v_pk_mul_f32 v[40:41], v[78:79], v[36:37] op_sel:[1,1] op_sel_hi:[1,0] neg_lo:[1,0]
	s_nop 0
	v_pk_fma_f32 v[40:41], v[78:79], v[36:37], v[40:41] op_sel_hi:[0,1,1]
	ds_write2_b64 v66, v[28:29], v[40:41] offset1:16
	v_pk_mul_f32 v[28:29], v[14:15], v[36:37] op_sel:[1,1] op_sel_hi:[0,1] neg_lo:[0,1]
	v_pk_fma_f32 v[28:29], v[14:15], v[36:37], v[28:29] op_sel_hi:[1,0,1]
	s_nop 0
	v_pk_mul_f32 v[36:37], v[32:33], v[28:29] op_sel:[1,1] op_sel_hi:[1,0] neg_lo:[1,0]
	s_nop 0
	v_pk_fma_f32 v[32:33], v[32:33], v[28:29], v[36:37] op_sel_hi:[0,1,1]
	v_pk_mul_f32 v[36:37], v[14:15], v[28:29] op_sel:[1,1] op_sel_hi:[0,1] neg_lo:[0,1]
	v_pk_fma_f32 v[28:29], v[14:15], v[28:29], v[36:37] op_sel_hi:[1,0,1]
	s_nop 0
	v_pk_mul_f32 v[36:37], v[50:51], v[28:29] op_sel:[1,1] op_sel_hi:[1,0] neg_lo:[1,0]
	s_nop 0
	v_pk_fma_f32 v[36:37], v[50:51], v[28:29], v[36:37] op_sel_hi:[0,1,1]
	ds_write2_b64 v65, v[32:33], v[36:37] offset0:32 offset1:48
	v_pk_mul_f32 v[32:33], v[14:15], v[28:29] op_sel:[1,1] op_sel_hi:[0,1] neg_lo:[0,1]
	v_pk_fma_f32 v[28:29], v[14:15], v[28:29], v[32:33] op_sel_hi:[1,0,1]
	s_nop 0
	v_pk_mul_f32 v[32:33], v[24:25], v[28:29] op_sel:[1,1] op_sel_hi:[1,0] neg_lo:[1,0]
	s_nop 0
	v_pk_fma_f32 v[24:25], v[24:25], v[28:29], v[32:33] op_sel_hi:[0,1,1]
	v_pk_mul_f32 v[32:33], v[14:15], v[28:29] op_sel:[1,1] op_sel_hi:[0,1] neg_lo:[0,1]
	v_pk_fma_f32 v[28:29], v[14:15], v[28:29], v[32:33] op_sel_hi:[1,0,1]
	s_nop 0
	v_pk_mul_f32 v[32:33], v[46:47], v[28:29] op_sel:[1,1] op_sel_hi:[1,0] neg_lo:[1,0]
	s_nop 0
	v_pk_fma_f32 v[32:33], v[46:47], v[28:29], v[32:33] op_sel_hi:[0,1,1]
	ds_write2_b64 v64, v[24:25], v[32:33] offset0:64 offset1:80
	v_pk_mul_f32 v[24:25], v[14:15], v[28:29] op_sel:[1,1] op_sel_hi:[0,1] neg_lo:[0,1]
	v_pk_fma_f32 v[24:25], v[14:15], v[28:29], v[24:25] op_sel_hi:[1,0,1]
	s_nop 0
	v_pk_mul_f32 v[28:29], v[26:27], v[24:25] op_sel:[1,1] op_sel_hi:[1,0] neg_lo:[1,0]
	s_nop 0
	v_pk_fma_f32 v[26:27], v[26:27], v[24:25], v[28:29] op_sel_hi:[0,1,1]
	v_pk_mul_f32 v[28:29], v[14:15], v[24:25] op_sel:[1,1] op_sel_hi:[0,1] neg_lo:[0,1]
	v_pk_fma_f32 v[24:25], v[14:15], v[24:25], v[28:29] op_sel_hi:[1,0,1]
	s_nop 0
	v_pk_mul_f32 v[28:29], v[80:81], v[24:25] op_sel:[1,1] op_sel_hi:[1,0] neg_lo:[1,0]
	s_nop 0
	v_pk_fma_f32 v[28:29], v[80:81], v[24:25], v[28:29] op_sel_hi:[0,1,1]
	ds_write2_b64 v63, v[26:27], v[28:29] offset0:96 offset1:112
	v_pk_mul_f32 v[26:27], v[14:15], v[24:25] op_sel:[1,1] op_sel_hi:[0,1] neg_lo:[0,1]
	v_pk_fma_f32 v[24:25], v[14:15], v[24:25], v[26:27] op_sel_hi:[1,0,1]
	s_nop 0
	v_pk_mul_f32 v[26:27], v[20:21], v[24:25] op_sel:[1,1] op_sel_hi:[1,0] neg_lo:[1,0]
	s_nop 0
	v_pk_fma_f32 v[20:21], v[20:21], v[24:25], v[26:27] op_sel_hi:[0,1,1]
	v_pk_mul_f32 v[26:27], v[14:15], v[24:25] op_sel:[1,1] op_sel_hi:[0,1] neg_lo:[0,1]
	v_pk_fma_f32 v[24:25], v[14:15], v[24:25], v[26:27] op_sel_hi:[1,0,1]
	s_nop 0
	v_pk_mul_f32 v[26:27], v[38:39], v[24:25] op_sel:[1,1] op_sel_hi:[1,0] neg_lo:[1,0]
	s_nop 0
	v_pk_fma_f32 v[26:27], v[38:39], v[24:25], v[26:27] op_sel_hi:[0,1,1]
	ds_write2_b64 v62, v[20:21], v[26:27] offset0:128 offset1:144
	v_pk_mul_f32 v[20:21], v[14:15], v[24:25] op_sel:[1,1] op_sel_hi:[0,1] neg_lo:[0,1]
	v_pk_fma_f32 v[20:21], v[14:15], v[24:25], v[20:21] op_sel_hi:[1,0,1]
	s_nop 0
	v_pk_mul_f32 v[24:25], v[22:23], v[20:21] op_sel:[1,1] op_sel_hi:[1,0] neg_lo:[1,0]
	s_nop 0
	v_pk_fma_f32 v[22:23], v[22:23], v[20:21], v[24:25] op_sel_hi:[0,1,1]
	v_pk_mul_f32 v[24:25], v[14:15], v[20:21] op_sel:[1,1] op_sel_hi:[0,1] neg_lo:[0,1]
	v_pk_fma_f32 v[20:21], v[14:15], v[20:21], v[24:25] op_sel_hi:[1,0,1]
	s_nop 0
	v_pk_mul_f32 v[24:25], v[42:43], v[20:21] op_sel:[1,1] op_sel_hi:[1,0] neg_lo:[1,0]
	s_nop 0
	v_pk_fma_f32 v[24:25], v[42:43], v[20:21], v[24:25] op_sel_hi:[0,1,1]
	ds_write2_b64 v61, v[22:23], v[24:25] offset0:160 offset1:176
	v_pk_mul_f32 v[22:23], v[14:15], v[20:21] op_sel:[1,1] op_sel_hi:[0,1] neg_lo:[0,1]
	v_pk_fma_f32 v[20:21], v[14:15], v[20:21], v[22:23] op_sel_hi:[1,0,1]
	s_nop 0
	v_pk_mul_f32 v[22:23], v[16:17], v[20:21] op_sel:[1,1] op_sel_hi:[1,0] neg_lo:[1,0]
	s_nop 0
	v_pk_fma_f32 v[16:17], v[16:17], v[20:21], v[22:23] op_sel_hi:[0,1,1]
	v_pk_mul_f32 v[22:23], v[14:15], v[20:21] op_sel:[1,1] op_sel_hi:[0,1] neg_lo:[0,1]
	v_pk_fma_f32 v[20:21], v[14:15], v[20:21], v[22:23] op_sel_hi:[1,0,1]
	s_nop 0
	v_pk_mul_f32 v[22:23], v[30:31], v[20:21] op_sel:[1,1] op_sel_hi:[1,0] neg_lo:[1,0]
	s_nop 0
	v_pk_fma_f32 v[22:23], v[30:31], v[20:21], v[22:23] op_sel_hi:[0,1,1]
	ds_write2_b64 v60, v[16:17], v[22:23] offset0:192 offset1:208
	v_pk_mul_f32 v[16:17], v[14:15], v[20:21] op_sel:[1,1] op_sel_hi:[0,1] neg_lo:[0,1]
	v_pk_fma_f32 v[16:17], v[14:15], v[20:21], v[16:17] op_sel_hi:[1,0,1]
	s_nop 0
	v_pk_mul_f32 v[20:21], v[18:19], v[16:17] op_sel:[1,1] op_sel_hi:[1,0] neg_lo:[1,0]
	s_nop 0
	v_pk_fma_f32 v[18:19], v[18:19], v[16:17], v[20:21] op_sel_hi:[0,1,1]
	v_pk_mul_f32 v[20:21], v[14:15], v[16:17] op_sel:[1,1] op_sel_hi:[0,1] neg_lo:[0,1]
	v_pk_fma_f32 v[14:15], v[14:15], v[16:17], v[20:21] op_sel_hi:[1,0,1]
	s_nop 0
	v_pk_mul_f32 v[16:17], v[34:35], v[14:15] op_sel:[1,1] op_sel_hi:[1,0] neg_lo:[1,0]
	s_nop 0
	v_pk_fma_f32 v[14:15], v[34:35], v[14:15], v[16:17] op_sel_hi:[0,1,1]
	ds_write2_b64 v13, v[18:19], v[14:15] offset0:224 offset1:240
	v_mov_b32_e32 v14, v182
	v_mov_b32_e32 v10, v176
	v_mov_b32_e32 v13, v175
	s_waitcnt lgkmcnt(0)
	s_barrier
	v_mov_b32_e32 v48, v167
	v_xor_b32_e32 v16, 1, v13
	v_lshlrev_b32_e32 v10, 3, v10
	v_lshlrev_b32_e32 v16, 3, v16
	v_add3_u32 v18, 0, v16, v10
	v_xor_b32_e32 v16, 2, v13
	v_lshlrev_b32_e32 v16, 3, v16
	v_xor_b32_e32 v24, 5, v13
	v_add3_u32 v20, 0, v16, v10
	v_xor_b32_e32 v16, 3, v13
	v_lshlrev_b32_e32 v24, 3, v24
	v_lshlrev_b32_e32 v15, 3, v13
	v_lshlrev_b32_e32 v16, 3, v16
	v_add3_u32 v26, 0, v24, v10
	v_xor_b32_e32 v24, 6, v13
	v_add3_u32 v15, 0, v15, v10
	v_add3_u32 v22, 0, v16, v10
	v_lshlrev_b32_e32 v24, 3, v24
	v_xor_b32_e32 v32, 9, v13
	ds_read_b64 v[16:17], v15
	ds_read_b64 v[18:19], v18
	ds_read_b64 v[20:21], v20
	ds_read_b64 v[22:23], v22
	v_xor_b32_e32 v15, 4, v13
	v_add3_u32 v28, 0, v24, v10
	v_xor_b32_e32 v24, 7, v13
	v_lshlrev_b32_e32 v32, 3, v32
	v_lshlrev_b32_e32 v15, 3, v15
	v_lshlrev_b32_e32 v24, 3, v24
	v_add3_u32 v34, 0, v32, v10
	v_xor_b32_e32 v32, 10, v13
	v_add3_u32 v15, 0, v15, v10
	v_add3_u32 v30, 0, v24, v10
	v_lshlrev_b32_e32 v32, 3, v32
	ds_read_b64 v[24:25], v15
	ds_read_b64 v[26:27], v26
	ds_read_b64 v[28:29], v28
	ds_read_b64 v[30:31], v30
	v_xor_b32_e32 v15, 8, v13
	v_add3_u32 v36, 0, v32, v10
	v_xor_b32_e32 v32, 11, v13
	v_lshlrev_b32_e32 v15, 3, v15
	v_lshlrev_b32_e32 v32, 3, v32
	v_xor_b32_e32 v40, 13, v13
	v_add3_u32 v15, 0, v15, v10
	v_add3_u32 v38, 0, v32, v10
	v_lshlrev_b32_e32 v40, 3, v40
	ds_read_b64 v[32:33], v15
	ds_read_b64 v[34:35], v34
	ds_read_b64 v[36:37], v36
	ds_read_b64 v[38:39], v38
	v_xor_b32_e32 v15, 12, v13
	v_add3_u32 v42, 0, v40, v10
	v_xor_b32_e32 v40, 14, v13
	v_xor_b32_e32 v13, 15, v13
	v_lshlrev_b32_e32 v15, 3, v15
	v_lshlrev_b32_e32 v40, 3, v40
	v_lshlrev_b32_e32 v13, 3, v13
	v_add3_u32 v15, 0, v15, v10
	v_add3_u32 v44, 0, v40, v10
	v_add3_u32 v10, 0, v13, v10
	ds_read_b64 v[40:41], v15
	ds_read_b64 v[42:43], v42
	ds_read_b64 v[44:45], v44
	ds_read_b64 v[46:47], v10
	v_mov_b32_e32 v10, v1
	v_mov_b32_e32 v13, v166
	v_mov_b32_e32 v10, v164
	s_waitcnt lgkmcnt(7)
	v_pk_add_f32 v[52:53], v[16:17], v[32:33]
	v_mov_b32_e32 v10, v165
	v_pk_add_f32 v[16:17], v[16:17], v[32:33] neg_lo:[0,1] neg_hi:[0,1]
	s_waitcnt lgkmcnt(6)
	v_pk_add_f32 v[32:33], v[18:19], v[34:35]
	v_pk_add_f32 v[18:19], v[18:19], v[34:35] neg_lo:[0,1] neg_hi:[0,1]
	v_mov_b32_e32 v13, v168
	v_mov_b32_e32 v50, v169
	v_ashrrev_i32_e32 v15, 31, v14
	v_pk_mul_f32 v[34:35], v[18:19], v[50:51] op_sel:[1,0] op_sel_hi:[0,0] neg_lo:[1,1] neg_hi:[0,1]
	v_mov_b32_e32 v13, v170
	v_pk_fma_f32 v[18:19], v[18:19], v[10:11], v[34:35] op_sel_hi:[1,0,1]
	s_waitcnt lgkmcnt(5)
	v_pk_add_f32 v[34:35], v[20:21], v[36:37]
	v_pk_add_f32 v[20:21], v[20:21], v[36:37] neg_lo:[0,1] neg_hi:[0,1]
	s_nop 0
	v_pk_mul_f32 v[36:37], v[20:21], v[48:49] op_sel:[1,0] op_sel_hi:[0,0] neg_lo:[1,1] neg_hi:[0,1]
	v_mov_b32_e32 v13, v171
	v_pk_fma_f32 v[20:21], v[20:21], v[48:49], v[36:37] op_sel_hi:[1,0,1]
	s_waitcnt lgkmcnt(4)
	v_pk_add_f32 v[36:37], v[22:23], v[38:39]
	v_pk_add_f32 v[22:23], v[22:23], v[38:39] neg_lo:[0,1] neg_hi:[0,1]
	s_nop 0
	v_pk_mul_f32 v[38:39], v[22:23], v[50:51] op_sel_hi:[1,0]
	s_nop 0
	v_pk_fma_f32 v[22:23], v[22:23], v[10:11], v[38:39] op_sel:[1,0,0] op_sel_hi:[0,0,1] neg_lo:[1,1,0] neg_hi:[0,1,0]
	s_waitcnt lgkmcnt(3)
	v_pk_add_f32 v[38:39], v[24:25], v[40:41]
	v_pk_add_f32 v[24:25], v[24:25], v[40:41] neg_lo:[0,1] neg_hi:[0,1]
	v_mov_b32_e32 v13, v175
	v_xor_b32_e32 v41, 0x80000000, v24
	v_mov_b32_e32 v40, v25
	s_waitcnt lgkmcnt(2)
	v_pk_add_f32 v[24:25], v[26:27], v[42:43]
	v_pk_add_f32 v[26:27], v[26:27], v[42:43] neg_lo:[0,1] neg_hi:[0,1]
	s_nop 0
	v_pk_mul_f32 v[42:43], v[26:27], v[50:51] op_sel_hi:[1,0] neg_lo:[0,1] neg_hi:[0,1]
	s_nop 0
	v_pk_fma_f32 v[26:27], v[26:27], v[10:11], v[42:43] op_sel:[1,0,0] op_sel_hi:[0,0,1] neg_lo:[1,1,0] neg_hi:[0,1,0]
	s_waitcnt lgkmcnt(1)
	v_pk_add_f32 v[42:43], v[28:29], v[44:45]
	v_pk_add_f32 v[28:29], v[28:29], v[44:45] neg_lo:[0,1] neg_hi:[0,1]
	s_nop 0
	v_pk_mul_f32 v[44:45], v[28:29], v[48:49] op_sel:[1,0] op_sel_hi:[0,0] neg_lo:[1,1] neg_hi:[0,1]
	s_nop 0
	v_pk_fma_f32 v[28:29], v[28:29], v[48:49], v[44:45] op_sel_hi:[1,0,1] neg_lo:[0,1,0] neg_hi:[0,1,0]
	s_waitcnt lgkmcnt(0)
	v_pk_add_f32 v[44:45], v[30:31], v[46:47]
	v_pk_add_f32 v[30:31], v[30:31], v[46:47] neg_lo:[0,1] neg_hi:[0,1]
	s_nop 0
	v_pk_mul_f32 v[46:47], v[30:31], v[50:51] op_sel:[1,0] op_sel_hi:[0,0] neg_lo:[1,1] neg_hi:[0,1]
	v_pk_add_f32 v[50:51], v[32:33], v[24:25]
	v_pk_add_f32 v[24:25], v[32:33], v[24:25] neg_lo:[0,1] neg_hi:[0,1]
	v_pk_fma_f32 v[30:31], v[30:31], v[10:11], v[46:47] op_sel_hi:[1,0,1] neg_lo:[0,1,0] neg_hi:[0,1,0]
	v_pk_mul_f32 v[32:33], v[24:25], v[48:49] op_sel:[1,0] op_sel_hi:[0,0] neg_lo:[1,1] neg_hi:[0,1]
	v_pk_add_f32 v[46:47], v[52:53], v[38:39]
	v_pk_fma_f32 v[24:25], v[24:25], v[48:49], v[32:33] op_sel_hi:[1,0,1]
	v_pk_add_f32 v[32:33], v[34:35], v[42:43]
	v_pk_add_f32 v[34:35], v[34:35], v[42:43] neg_lo:[0,1] neg_hi:[0,1]
	v_pk_add_f32 v[38:39], v[52:53], v[38:39] neg_lo:[0,1] neg_hi:[0,1]
	v_xor_b32_e32 v43, 0x80000000, v34
	v_mov_b32_e32 v42, v35
	v_pk_add_f32 v[34:35], v[36:37], v[44:45]
	v_pk_add_f32 v[36:37], v[36:37], v[44:45] neg_lo:[0,1] neg_hi:[0,1]
	v_mov_b32_e32 v10, v177
	v_pk_mul_f32 v[44:45], v[36:37], v[48:49] op_sel:[1,0] op_sel_hi:[0,0] neg_lo:[1,1] neg_hi:[0,1]
	s_nop 0
	v_pk_fma_f32 v[36:37], v[36:37], v[48:49], v[44:45] op_sel_hi:[1,0,1] neg_lo:[0,1,0] neg_hi:[0,1,0]
	v_pk_add_f32 v[44:45], v[46:47], v[32:33]
	v_pk_add_f32 v[32:33], v[46:47], v[32:33] neg_lo:[0,1] neg_hi:[0,1]
	v_pk_add_f32 v[46:47], v[50:51], v[34:35]
	v_pk_add_f32 v[34:35], v[50:51], v[34:35] neg_lo:[0,1] neg_hi:[0,1]
	s_nop 0
	v_xor_b32_e32 v51, 0x80000000, v34
	v_mov_b32_e32 v50, v35
	v_pk_add_f32 v[34:35], v[44:45], v[46:47]
	v_pk_add_f32 v[44:45], v[44:45], v[46:47] neg_lo:[0,1] neg_hi:[0,1]
	v_pk_add_f32 v[46:47], v[32:33], v[50:51]
	v_pk_add_f32 v[32:33], v[32:33], v[50:51] neg_lo:[0,1] neg_hi:[0,1]
	v_pk_add_f32 v[50:51], v[38:39], v[42:43]
	v_pk_add_f32 v[38:39], v[38:39], v[42:43] neg_lo:[0,1] neg_hi:[0,1]
	v_pk_add_f32 v[42:43], v[24:25], v[36:37]
	v_pk_add_f32 v[24:25], v[24:25], v[36:37] neg_lo:[0,1] neg_hi:[0,1]
	s_nop 0
	v_xor_b32_e32 v37, 0x80000000, v24
	v_mov_b32_e32 v36, v25
	v_pk_add_f32 v[24:25], v[50:51], v[42:43]
	v_pk_add_f32 v[42:43], v[50:51], v[42:43] neg_lo:[0,1] neg_hi:[0,1]
	v_pk_add_f32 v[50:51], v[38:39], v[36:37]
	v_pk_add_f32 v[36:37], v[38:39], v[36:37] neg_lo:[0,1] neg_hi:[0,1]
	v_pk_add_f32 v[38:39], v[16:17], v[40:41]
	v_pk_add_f32 v[16:17], v[16:17], v[40:41] neg_lo:[0,1] neg_hi:[0,1]
	v_pk_add_f32 v[40:41], v[18:19], v[26:27]
	v_pk_add_f32 v[18:19], v[18:19], v[26:27] neg_lo:[0,1] neg_hi:[0,1]
	s_nop 0
	v_pk_mul_f32 v[26:27], v[48:49], v[18:19] op_sel:[0,1] op_sel_hi:[0,0] neg_lo:[1,1] neg_hi:[1,0]
	v_pk_fma_f32 v[18:19], v[48:49], v[18:19], v[26:27] op_sel_hi:[0,1,1]
	v_pk_add_f32 v[26:27], v[20:21], v[28:29]
	v_pk_add_f32 v[20:21], v[20:21], v[28:29] neg_lo:[0,1] neg_hi:[0,1]
	s_nop 0
	v_xor_b32_e32 v29, 0x80000000, v20
	v_mov_b32_e32 v28, v21
	v_pk_add_f32 v[20:21], v[22:23], v[30:31]
	v_pk_add_f32 v[22:23], v[22:23], v[30:31] neg_lo:[0,1] neg_hi:[0,1]
	s_nop 0
	v_pk_mul_f32 v[30:31], v[48:49], v[22:23] op_sel:[0,1] op_sel_hi:[0,0] neg_lo:[1,1] neg_hi:[1,0]
	v_pk_fma_f32 v[22:23], v[48:49], v[22:23], v[30:31] op_sel_hi:[0,1,1] neg_lo:[1,0,0] neg_hi:[1,0,0]
	v_pk_add_f32 v[30:31], v[38:39], v[26:27]
	v_pk_add_f32 v[26:27], v[38:39], v[26:27] neg_lo:[0,1] neg_hi:[0,1]
	v_pk_add_f32 v[38:39], v[40:41], v[20:21]
	v_pk_add_f32 v[20:21], v[40:41], v[20:21] neg_lo:[0,1] neg_hi:[0,1]
	v_mov_b32_e32 v48, v167
	v_xor_b32_e32 v41, 0x80000000, v20
	v_mov_b32_e32 v40, v21
	v_pk_add_f32 v[20:21], v[30:31], v[38:39]
	v_pk_add_f32 v[30:31], v[30:31], v[38:39] neg_lo:[0,1] neg_hi:[0,1]
	v_pk_add_f32 v[38:39], v[26:27], v[40:41]
	v_pk_add_f32 v[26:27], v[26:27], v[40:41] neg_lo:[0,1] neg_hi:[0,1]
	v_pk_add_f32 v[40:41], v[16:17], v[28:29]
	v_pk_add_f32 v[16:17], v[16:17], v[28:29] neg_lo:[0,1] neg_hi:[0,1]
	v_pk_add_f32 v[28:29], v[18:19], v[22:23]
	v_pk_add_f32 v[18:19], v[18:19], v[22:23] neg_lo:[0,1] neg_hi:[0,1]
	s_nop 0
	v_xor_b32_e32 v23, 0x80000000, v18
	v_mov_b32_e32 v22, v19
	v_pk_add_f32 v[18:19], v[40:41], v[28:29]
	v_pk_add_f32 v[28:29], v[40:41], v[28:29] neg_lo:[0,1] neg_hi:[0,1]
	v_pk_add_f32 v[40:41], v[16:17], v[22:23]
	v_pk_add_f32 v[16:17], v[16:17], v[22:23] neg_lo:[0,1] neg_hi:[0,1]
	v_lshl_add_u64 v[22:23], v[14:15], 3, s[46:47]
	global_store_dwordx2 v[22:23], v[34:35], off
	v_add_u32_e32 v22, 0x200, v14
	v_ashrrev_i32_e32 v23, 31, v22
	v_lshl_add_u64 v[22:23], v[22:23], 3, s[46:47]
	global_store_dwordx2 v[22:23], v[20:21], off
	v_add_u32_e32 v20, 0x400, v14
	v_ashrrev_i32_e32 v21, 31, v20
	v_lshl_add_u64 v[20:21], v[20:21], 3, s[46:47]
	global_store_dwordx2 v[20:21], v[24:25], off
	v_add_u32_e32 v20, 0x600, v14
	v_ashrrev_i32_e32 v21, 31, v20
	v_lshl_add_u64 v[20:21], v[20:21], 3, s[46:47]
	global_store_dwordx2 v[20:21], v[18:19], off
	v_add_u32_e32 v18, 0x800, v14
	v_ashrrev_i32_e32 v19, 31, v18
	v_lshl_add_u64 v[18:19], v[18:19], 3, s[46:47]
	global_store_dwordx2 v[18:19], v[46:47], off
	v_add_u32_e32 v18, 0xa00, v14
	v_ashrrev_i32_e32 v19, 31, v18
	v_lshl_add_u64 v[18:19], v[18:19], 3, s[46:47]
	global_store_dwordx2 v[18:19], v[38:39], off
	v_add_u32_e32 v18, 0xc00, v14
	v_ashrrev_i32_e32 v19, 31, v18
	v_lshl_add_u64 v[18:19], v[18:19], 3, s[46:47]
	global_store_dwordx2 v[18:19], v[50:51], off
	v_add_u32_e32 v18, 0xe00, v14
	v_ashrrev_i32_e32 v19, 31, v18
	v_lshl_add_u64 v[18:19], v[18:19], 3, s[46:47]
	global_store_dwordx2 v[18:19], v[40:41], off
	v_add_u32_e32 v18, 0x1000, v14
	v_ashrrev_i32_e32 v19, 31, v18
	v_lshl_add_u64 v[18:19], v[18:19], 3, s[46:47]
	global_store_dwordx2 v[18:19], v[44:45], off
	v_add_u32_e32 v18, 0x1200, v14
	v_ashrrev_i32_e32 v19, 31, v18
	v_lshl_add_u64 v[18:19], v[18:19], 3, s[46:47]
	global_store_dwordx2 v[18:19], v[30:31], off
	v_add_u32_e32 v18, 0x1400, v14
	v_ashrrev_i32_e32 v19, 31, v18
	v_lshl_add_u64 v[18:19], v[18:19], 3, s[46:47]
	global_store_dwordx2 v[18:19], v[42:43], off
	v_add_u32_e32 v18, 0x1600, v14
	v_ashrrev_i32_e32 v19, 31, v18
	v_lshl_add_u64 v[18:19], v[18:19], 3, s[46:47]
	global_store_dwordx2 v[18:19], v[28:29], off
	v_add_u32_e32 v18, 0x1800, v14
	v_ashrrev_i32_e32 v19, 31, v18
	v_lshl_add_u64 v[18:19], v[18:19], 3, s[46:47]
	global_store_dwordx2 v[18:19], v[32:33], off
	v_add_u32_e32 v18, 0x1a00, v14
	v_ashrrev_i32_e32 v19, 31, v18
	v_lshl_add_u64 v[18:19], v[18:19], 3, s[46:47]
	global_store_dwordx2 v[18:19], v[26:27], off
	v_add_u32_e32 v18, 0x1c00, v14
	v_ashrrev_i32_e32 v19, 31, v18
	v_lshl_add_u64 v[18:19], v[18:19], 3, s[46:47]
	global_store_dwordx2 v[18:19], v[36:37], off
	v_add_u32_e32 v18, 0x1e00, v14
	v_ashrrev_i32_e32 v19, 31, v18
	v_lshl_add_u64 v[18:19], v[18:19], 3, s[46:47]
	global_store_dwordx2 v[18:19], v[16:17], off
	v_mov_b32_e32 v50, v169
	v_xor_b32_e32 v16, 1, v13
	v_lshlrev_b32_e32 v10, 3, v10
	v_lshlrev_b32_e32 v16, 3, v16
	v_add3_u32 v18, 0, v16, v10
	v_xor_b32_e32 v16, 2, v13
	v_lshlrev_b32_e32 v16, 3, v16
	v_xor_b32_e32 v24, 5, v13
	v_add3_u32 v20, 0, v16, v10
	v_xor_b32_e32 v16, 3, v13
	v_lshlrev_b32_e32 v24, 3, v24
	v_lshlrev_b32_e32 v15, 3, v13
	v_lshlrev_b32_e32 v16, 3, v16
	v_add3_u32 v26, 0, v24, v10
	v_xor_b32_e32 v24, 6, v13
	v_add3_u32 v15, 0, v15, v10
	v_add3_u32 v22, 0, v16, v10
	v_lshlrev_b32_e32 v24, 3, v24
	v_xor_b32_e32 v32, 9, v13
	ds_read_b64 v[16:17], v15
	ds_read_b64 v[18:19], v18
	ds_read_b64 v[20:21], v20
	ds_read_b64 v[22:23], v22
	v_xor_b32_e32 v15, 4, v13
	v_add3_u32 v28, 0, v24, v10
	v_xor_b32_e32 v24, 7, v13
	v_lshlrev_b32_e32 v32, 3, v32
	v_lshlrev_b32_e32 v15, 3, v15
	v_lshlrev_b32_e32 v24, 3, v24
	v_add3_u32 v34, 0, v32, v10
	v_xor_b32_e32 v32, 10, v13
	v_add3_u32 v15, 0, v15, v10
	v_add3_u32 v30, 0, v24, v10
	v_lshlrev_b32_e32 v32, 3, v32
	ds_read_b64 v[24:25], v15
	ds_read_b64 v[26:27], v26
	ds_read_b64 v[28:29], v28
	ds_read_b64 v[30:31], v30
	v_xor_b32_e32 v15, 8, v13
	v_add3_u32 v36, 0, v32, v10
	v_xor_b32_e32 v32, 11, v13
	v_lshlrev_b32_e32 v15, 3, v15
	v_lshlrev_b32_e32 v32, 3, v32
	v_xor_b32_e32 v40, 13, v13
	v_add3_u32 v15, 0, v15, v10
	v_add3_u32 v38, 0, v32, v10
	v_lshlrev_b32_e32 v40, 3, v40
	ds_read_b64 v[32:33], v15
	ds_read_b64 v[34:35], v34
	ds_read_b64 v[36:37], v36
	ds_read_b64 v[38:39], v38
	v_xor_b32_e32 v15, 12, v13
	v_add3_u32 v42, 0, v40, v10
	v_xor_b32_e32 v40, 14, v13
	v_xor_b32_e32 v13, 15, v13
	v_lshlrev_b32_e32 v15, 3, v15
	v_lshlrev_b32_e32 v40, 3, v40
	v_lshlrev_b32_e32 v13, 3, v13
	v_add3_u32 v15, 0, v15, v10
	v_add3_u32 v44, 0, v40, v10
	v_add3_u32 v10, 0, v13, v10
	ds_read_b64 v[40:41], v15
	ds_read_b64 v[42:43], v42
	ds_read_b64 v[44:45], v44
	ds_read_b64 v[46:47], v10
	v_mov_b32_e32 v10, v1
	v_mov_b32_e32 v13, v166
	v_mov_b32_e32 v10, v164
	s_waitcnt lgkmcnt(7)
	v_pk_add_f32 v[52:53], v[16:17], v[32:33]
	v_mov_b32_e32 v10, v165
	v_pk_add_f32 v[16:17], v[16:17], v[32:33] neg_lo:[0,1] neg_hi:[0,1]
	s_waitcnt lgkmcnt(6)
	v_pk_add_f32 v[32:33], v[18:19], v[34:35]
	v_pk_add_f32 v[18:19], v[18:19], v[34:35] neg_lo:[0,1] neg_hi:[0,1]
	v_mov_b32_e32 v13, v168
	s_nop 0
	v_pk_mul_f32 v[34:35], v[18:19], v[50:51] op_sel:[1,0] op_sel_hi:[0,0] neg_lo:[1,1] neg_hi:[0,1]
	v_mov_b32_e32 v13, v170
	v_pk_fma_f32 v[18:19], v[18:19], v[10:11], v[34:35] op_sel_hi:[1,0,1]
	s_waitcnt lgkmcnt(5)
	v_pk_add_f32 v[34:35], v[20:21], v[36:37]
	v_pk_add_f32 v[20:21], v[20:21], v[36:37] neg_lo:[0,1] neg_hi:[0,1]
	s_nop 0
	v_pk_mul_f32 v[36:37], v[20:21], v[48:49] op_sel:[1,0] op_sel_hi:[0,0] neg_lo:[1,1] neg_hi:[0,1]
	v_mov_b32_e32 v13, v171
	v_pk_fma_f32 v[20:21], v[20:21], v[48:49], v[36:37] op_sel_hi:[1,0,1]
	s_waitcnt lgkmcnt(4)
	v_pk_add_f32 v[36:37], v[22:23], v[38:39]
	v_pk_add_f32 v[22:23], v[22:23], v[38:39] neg_lo:[0,1] neg_hi:[0,1]
	s_nop 0
	v_pk_mul_f32 v[38:39], v[22:23], v[50:51] op_sel_hi:[1,0]
	s_nop 0
	v_pk_fma_f32 v[22:23], v[22:23], v[10:11], v[38:39] op_sel:[1,0,0] op_sel_hi:[0,0,1] neg_lo:[1,1,0] neg_hi:[0,1,0]
	s_waitcnt lgkmcnt(3)
	v_pk_add_f32 v[38:39], v[24:25], v[40:41]
	v_pk_add_f32 v[24:25], v[24:25], v[40:41] neg_lo:[0,1] neg_hi:[0,1]
	v_mov_b32_e32 v13, v173
	v_xor_b32_e32 v41, 0x80000000, v24
	v_mov_b32_e32 v40, v25
	s_waitcnt lgkmcnt(2)
	v_pk_add_f32 v[24:25], v[26:27], v[42:43]
	v_pk_add_f32 v[26:27], v[26:27], v[42:43] neg_lo:[0,1] neg_hi:[0,1]
	s_nop 0
	v_pk_mul_f32 v[42:43], v[26:27], v[50:51] op_sel_hi:[1,0] neg_lo:[0,1] neg_hi:[0,1]
	s_nop 0
	v_pk_fma_f32 v[26:27], v[26:27], v[10:11], v[42:43] op_sel:[1,0,0] op_sel_hi:[0,0,1] neg_lo:[1,1,0] neg_hi:[0,1,0]
	s_waitcnt lgkmcnt(1)
	v_pk_add_f32 v[42:43], v[28:29], v[44:45]
	v_pk_add_f32 v[28:29], v[28:29], v[44:45] neg_lo:[0,1] neg_hi:[0,1]
	s_nop 0
	v_pk_mul_f32 v[44:45], v[28:29], v[48:49] op_sel:[1,0] op_sel_hi:[0,0] neg_lo:[1,1] neg_hi:[0,1]
	s_nop 0
	v_pk_fma_f32 v[28:29], v[28:29], v[48:49], v[44:45] op_sel_hi:[1,0,1] neg_lo:[0,1,0] neg_hi:[0,1,0]
	s_waitcnt lgkmcnt(0)
	v_pk_add_f32 v[44:45], v[30:31], v[46:47]
	v_pk_add_f32 v[30:31], v[30:31], v[46:47] neg_lo:[0,1] neg_hi:[0,1]
	s_nop 0
	v_pk_mul_f32 v[46:47], v[30:31], v[50:51] op_sel:[1,0] op_sel_hi:[0,0] neg_lo:[1,1] neg_hi:[0,1]
	v_pk_add_f32 v[50:51], v[32:33], v[24:25]
	v_pk_add_f32 v[24:25], v[32:33], v[24:25] neg_lo:[0,1] neg_hi:[0,1]
	v_pk_fma_f32 v[30:31], v[30:31], v[10:11], v[46:47] op_sel_hi:[1,0,1] neg_lo:[0,1,0] neg_hi:[0,1,0]
	v_pk_mul_f32 v[32:33], v[24:25], v[48:49] op_sel:[1,0] op_sel_hi:[0,0] neg_lo:[1,1] neg_hi:[0,1]
	v_pk_add_f32 v[46:47], v[52:53], v[38:39]
	v_pk_fma_f32 v[24:25], v[24:25], v[48:49], v[32:33] op_sel_hi:[1,0,1]
	v_pk_add_f32 v[32:33], v[34:35], v[42:43]
	v_pk_add_f32 v[34:35], v[34:35], v[42:43] neg_lo:[0,1] neg_hi:[0,1]
	v_pk_add_f32 v[38:39], v[52:53], v[38:39] neg_lo:[0,1] neg_hi:[0,1]
	v_xor_b32_e32 v43, 0x80000000, v34
	v_mov_b32_e32 v42, v35
	v_pk_add_f32 v[34:35], v[36:37], v[44:45]
	v_pk_add_f32 v[36:37], v[36:37], v[44:45] neg_lo:[0,1] neg_hi:[0,1]
	v_mov_b32_e32 v10, v183
	v_pk_mul_f32 v[44:45], v[36:37], v[48:49] op_sel:[1,0] op_sel_hi:[0,0] neg_lo:[1,1] neg_hi:[0,1]
	s_nop 0
	v_pk_fma_f32 v[36:37], v[36:37], v[48:49], v[44:45] op_sel_hi:[1,0,1] neg_lo:[0,1,0] neg_hi:[0,1,0]
	v_pk_add_f32 v[44:45], v[46:47], v[32:33]
	v_pk_add_f32 v[32:33], v[46:47], v[32:33] neg_lo:[0,1] neg_hi:[0,1]
	v_pk_add_f32 v[46:47], v[50:51], v[34:35]
	v_pk_add_f32 v[34:35], v[50:51], v[34:35] neg_lo:[0,1] neg_hi:[0,1]
	s_nop 0
	v_xor_b32_e32 v51, 0x80000000, v34
	v_mov_b32_e32 v50, v35
	v_pk_add_f32 v[34:35], v[44:45], v[46:47]
	v_pk_add_f32 v[44:45], v[44:45], v[46:47] neg_lo:[0,1] neg_hi:[0,1]
	v_pk_add_f32 v[46:47], v[32:33], v[50:51]
	v_pk_add_f32 v[32:33], v[32:33], v[50:51] neg_lo:[0,1] neg_hi:[0,1]
	v_pk_add_f32 v[50:51], v[38:39], v[42:43]
	v_pk_add_f32 v[38:39], v[38:39], v[42:43] neg_lo:[0,1] neg_hi:[0,1]
	v_pk_add_f32 v[42:43], v[24:25], v[36:37]
	v_pk_add_f32 v[24:25], v[24:25], v[36:37] neg_lo:[0,1] neg_hi:[0,1]
	s_nop 0
	v_xor_b32_e32 v37, 0x80000000, v24
	v_mov_b32_e32 v36, v25
	v_pk_add_f32 v[24:25], v[50:51], v[42:43]
	v_pk_add_f32 v[42:43], v[50:51], v[42:43] neg_lo:[0,1] neg_hi:[0,1]
	v_pk_add_f32 v[50:51], v[38:39], v[36:37]
	v_pk_add_f32 v[36:37], v[38:39], v[36:37] neg_lo:[0,1] neg_hi:[0,1]
	v_pk_add_f32 v[38:39], v[16:17], v[40:41]
	v_pk_add_f32 v[16:17], v[16:17], v[40:41] neg_lo:[0,1] neg_hi:[0,1]
	v_pk_add_f32 v[40:41], v[18:19], v[26:27]
	v_pk_add_f32 v[18:19], v[18:19], v[26:27] neg_lo:[0,1] neg_hi:[0,1]
	s_nop 0
	v_pk_mul_f32 v[26:27], v[48:49], v[18:19] op_sel:[0,1] op_sel_hi:[0,0] neg_lo:[1,1] neg_hi:[1,0]
	v_pk_fma_f32 v[18:19], v[48:49], v[18:19], v[26:27] op_sel_hi:[0,1,1]
	v_pk_add_f32 v[26:27], v[20:21], v[28:29]
	v_pk_add_f32 v[20:21], v[20:21], v[28:29] neg_lo:[0,1] neg_hi:[0,1]
	s_nop 0
	v_xor_b32_e32 v29, 0x80000000, v20
	v_mov_b32_e32 v28, v21
	v_pk_add_f32 v[20:21], v[22:23], v[30:31]
	v_pk_add_f32 v[22:23], v[22:23], v[30:31] neg_lo:[0,1] neg_hi:[0,1]
	s_nop 0
	v_pk_mul_f32 v[30:31], v[48:49], v[22:23] op_sel:[0,1] op_sel_hi:[0,0] neg_lo:[1,1] neg_hi:[1,0]
	v_pk_fma_f32 v[22:23], v[48:49], v[22:23], v[30:31] op_sel_hi:[0,1,1] neg_lo:[1,0,0] neg_hi:[1,0,0]
	v_pk_add_f32 v[30:31], v[38:39], v[26:27]
	v_pk_add_f32 v[26:27], v[38:39], v[26:27] neg_lo:[0,1] neg_hi:[0,1]
	v_pk_add_f32 v[38:39], v[40:41], v[20:21]
	v_pk_add_f32 v[20:21], v[40:41], v[20:21] neg_lo:[0,1] neg_hi:[0,1]
	s_nop 0
	v_xor_b32_e32 v41, 0x80000000, v20
	v_mov_b32_e32 v40, v21
	v_pk_add_f32 v[20:21], v[30:31], v[38:39]
	v_pk_add_f32 v[30:31], v[30:31], v[38:39] neg_lo:[0,1] neg_hi:[0,1]
	v_pk_add_f32 v[38:39], v[26:27], v[40:41]
	v_pk_add_f32 v[26:27], v[26:27], v[40:41] neg_lo:[0,1] neg_hi:[0,1]
	v_pk_add_f32 v[40:41], v[16:17], v[28:29]
	v_pk_add_f32 v[16:17], v[16:17], v[28:29] neg_lo:[0,1] neg_hi:[0,1]
	v_pk_add_f32 v[28:29], v[18:19], v[22:23]
	v_pk_add_f32 v[18:19], v[18:19], v[22:23] neg_lo:[0,1] neg_hi:[0,1]
	s_nop 0
	v_xor_b32_e32 v23, 0x80000000, v18
	v_mov_b32_e32 v22, v19
	v_pk_add_f32 v[18:19], v[40:41], v[28:29]
	v_pk_add_f32 v[28:29], v[40:41], v[28:29] neg_lo:[0,1] neg_hi:[0,1]
	v_pk_add_f32 v[40:41], v[16:17], v[22:23]
	v_pk_add_f32 v[16:17], v[16:17], v[22:23] neg_lo:[0,1] neg_hi:[0,1]
	v_add_u32_e32 v22, 0x2000, v14
	v_ashrrev_i32_e32 v23, 31, v22
	v_lshl_add_u64 v[22:23], v[22:23], 3, s[46:47]
	global_store_dwordx2 v[22:23], v[34:35], off
	v_add_u32_e32 v22, 0x2200, v14
	v_ashrrev_i32_e32 v23, 31, v22
	v_lshl_add_u64 v[22:23], v[22:23], 3, s[46:47]
	global_store_dwordx2 v[22:23], v[20:21], off
	v_add_u32_e32 v20, 0x2400, v14
	v_ashrrev_i32_e32 v21, 31, v20
	v_lshl_add_u64 v[20:21], v[20:21], 3, s[46:47]
	global_store_dwordx2 v[20:21], v[24:25], off
	v_add_u32_e32 v20, 0x2600, v14
	v_ashrrev_i32_e32 v21, 31, v20
	v_lshl_add_u64 v[20:21], v[20:21], 3, s[46:47]
	global_store_dwordx2 v[20:21], v[18:19], off
	v_add_u32_e32 v18, 0x2800, v14
	v_ashrrev_i32_e32 v19, 31, v18
	v_lshl_add_u64 v[18:19], v[18:19], 3, s[46:47]
	global_store_dwordx2 v[18:19], v[46:47], off
	v_add_u32_e32 v18, 0x2a00, v14
	v_ashrrev_i32_e32 v19, 31, v18
	v_lshl_add_u64 v[18:19], v[18:19], 3, s[46:47]
	global_store_dwordx2 v[18:19], v[38:39], off
	v_add_u32_e32 v18, 0x2c00, v14
	v_ashrrev_i32_e32 v19, 31, v18
	v_lshl_add_u64 v[18:19], v[18:19], 3, s[46:47]
	global_store_dwordx2 v[18:19], v[50:51], off
	v_add_u32_e32 v18, 0x2e00, v14
	v_ashrrev_i32_e32 v19, 31, v18
	v_lshl_add_u64 v[18:19], v[18:19], 3, s[46:47]
	global_store_dwordx2 v[18:19], v[40:41], off
	v_add_u32_e32 v18, 0x3000, v14
	v_ashrrev_i32_e32 v19, 31, v18
	v_lshl_add_u64 v[18:19], v[18:19], 3, s[46:47]
	global_store_dwordx2 v[18:19], v[44:45], off
	v_add_u32_e32 v18, 0x3200, v14
	v_ashrrev_i32_e32 v19, 31, v18
	v_lshl_add_u64 v[18:19], v[18:19], 3, s[46:47]
	global_store_dwordx2 v[18:19], v[30:31], off
	v_add_u32_e32 v18, 0x3400, v14
	v_ashrrev_i32_e32 v19, 31, v18
	v_lshl_add_u64 v[18:19], v[18:19], 3, s[46:47]
	global_store_dwordx2 v[18:19], v[42:43], off
	v_add_u32_e32 v18, 0x3600, v14
	v_ashrrev_i32_e32 v19, 31, v18
	v_lshl_add_u64 v[18:19], v[18:19], 3, s[46:47]
	global_store_dwordx2 v[18:19], v[28:29], off
	v_add_u32_e32 v18, 0x3800, v14
	v_ashrrev_i32_e32 v19, 31, v18
	v_lshl_add_u64 v[18:19], v[18:19], 3, s[46:47]
	global_store_dwordx2 v[18:19], v[32:33], off
	v_add_u32_e32 v18, 0x3a00, v14
	v_ashrrev_i32_e32 v19, 31, v18
	v_lshl_add_u64 v[18:19], v[18:19], 3, s[46:47]
	global_store_dwordx2 v[18:19], v[26:27], off
	v_add_u32_e32 v18, 0x3c00, v14
	v_add_u32_e32 v14, 0x3e00, v14
	v_ashrrev_i32_e32 v15, 31, v14
	v_ashrrev_i32_e32 v19, 31, v18
	v_lshl_add_u64 v[14:15], v[14:15], 3, s[46:47]
	v_lshl_add_u64 v[18:19], v[18:19], 3, s[46:47]
	global_store_dwordx2 v[14:15], v[16:17], off
	v_mov_b32_e32 v16, v184
	v_mov_b32_e32 v14, v182
	global_store_dwordx2 v[18:19], v[36:37], off
	s_barrier
	s_nop 0
	v_pk_mul_f32 v[36:37], v[16:17], s[64:65] op_sel_hi:[0,1] neg_lo:[1,0]
	s_mov_b64 s[64:65], vcc
	v_ashrrev_i32_e32 v15, 31, v14
	v_lshl_add_u64 v[18:19], v[14:15], 2, s[64:65]
	s_movk_i32 vcc_lo, 0x1000
	v_add_co_u32_e32 v28, vcc, vcc_lo, v18
	v_pk_mul_f32 v[40:41], v[16:17], s[78:79] op_sel_hi:[0,1] neg_lo:[1,0]
	s_nop 0
	v_addc_co_u32_e32 v29, vcc, 0, v19, vcc
	v_add_co_u32_e32 v20, vcc, s39, v18
	s_movk_i32 s78, 0x3000
	s_nop 0
	v_addc_co_u32_e32 v21, vcc, 0, v19, vcc
	v_add_co_u32_e32 v48, vcc, s78, v18
	v_pk_mul_f32 v[32:33], v[16:17], s[40:41] op_sel_hi:[0,1] neg_lo:[1,0]
	s_nop 0
	v_addc_co_u32_e32 v49, vcc, 0, v19, vcc
	v_add_co_u32_e32 v22, vcc, s72, v18
	s_mov_b32 s40, 0x3f7ec46d
	s_nop 0
	v_addc_co_u32_e32 v23, vcc, 0, v19, vcc
	v_add_co_u32_e32 v58, vcc, s33, v18
	s_mov_b32 s33, 0x8000
	s_nop 0
	v_addc_co_u32_e32 v59, vcc, 0, v19, vcc
	v_add_co_u32_e32 v60, vcc, s43, v18
	s_mov_b32 s41, 0xbdc8bd36
	s_nop 0
	v_addc_co_u32_e32 v61, vcc, 0, v19, vcc
	v_add_co_u32_e32 v64, vcc, s73, v18
	v_pk_mul_f32 v[34:35], v[16:17], s[76:77] op_sel_hi:[0,1] neg_lo:[1,0]
	s_nop 0
	v_addc_co_u32_e32 v65, vcc, 0, v19, vcc
	v_add_co_u32_e32 v68, vcc, s33, v18
	s_mov_b32 s33, 0x9000
	s_nop 0
	v_addc_co_u32_e32 v69, vcc, 0, v19, vcc
	v_add_co_u32_e32 v24, vcc, s33, v18
	s_mov_b32 s33, 0xa000
	s_nop 0
	v_addc_co_u32_e32 v25, vcc, 0, v19, vcc
	v_add_co_u32_e32 v26, vcc, s33, v18
	s_mov_b32 s33, 0xb000
	s_nop 0
	v_addc_co_u32_e32 v27, vcc, 0, v19, vcc
	v_add_co_u32_e32 v30, vcc, s33, v18
	s_mov_b32 s33, 0xc000
	s_nop 0
	v_addc_co_u32_e32 v31, vcc, 0, v19, vcc
	v_add_co_u32_e32 v38, vcc, s33, v18
	s_mov_b32 s33, 0xd000
	s_nop 0
	v_addc_co_u32_e32 v39, vcc, 0, v19, vcc
	v_add_co_u32_e32 v44, vcc, s33, v18
	s_mov_b32 s33, 0xe000
	s_nop 0
	v_addc_co_u32_e32 v45, vcc, 0, v19, vcc
	v_add_co_u32_e32 v50, vcc, s33, v18
	s_mov_b32 s33, 0xf000
	s_nop 0
	v_addc_co_u32_e32 v51, vcc, 0, v19, vcc
	v_add_co_u32_e32 v70, vcc, s33, v18
	v_pk_mul_f32 v[92:93], v[16:17], s[62:63] op_sel_hi:[0,1] neg_lo:[1,0]
	s_nop 0
	v_addc_co_u32_e32 v71, vcc, 0, v19, vcc
	global_load_dword v94, v[68:69], off
	global_load_dword v96, v[68:69], off offset:2048
	global_load_dword v98, v[26:27], off offset:-4096
	global_load_dword v100, v[24:25], off offset:2048
	global_load_dword v102, v[26:27], off
	global_load_dword v104, v[26:27], off offset:2048
	global_load_dword v106, v[38:39], off offset:-4096
	global_load_dword v108, v[30:31], off offset:2048
	global_load_dword v110, v[38:39], off
	global_load_dword v112, v[38:39], off offset:2048
	global_load_dword v114, v[50:51], off offset:-4096
	global_load_dword v116, v[44:45], off offset:2048
	global_load_dword v118, v[50:51], off
	global_load_dword v120, v[50:51], off offset:2048
	global_load_dword v122, v[70:71], off
	global_load_dword v56, v[20:21], off
	s_nop 0
	global_load_dword v50, v[20:21], off offset:2048
	global_load_dword v124, v[70:71], off offset:2048
	global_load_dword v44, v[22:23], off offset:-4096
	global_load_dword v38, v[22:23], off
	global_load_dword v72, v[20:21], off offset:-4096
	global_load_dword v30, v[22:23], off offset:2048
	global_load_dword v26, v[60:61], off offset:-4096
	global_load_dword v24, v[60:61], off
	s_nop 0
	global_load_dword v22, v[60:61], off offset:2048
	global_load_dword v20, v[68:69], off offset:-4096
	global_load_dword v74, v[18:19], off
	global_load_dword v78, v[18:19], off offset:2048
	s_nop 0
	global_load_dword v68, v[28:29], off offset:2048
	s_nop 0
	global_load_dword v48, v[48:49], off offset:2048
	s_nop 0
	global_load_dword v28, v[58:59], off offset:2048
	global_load_dword v18, v[64:65], off offset:2048
	v_pk_mul_f32 v[52:53], v[16:17], s[58:59] op_sel_hi:[0,1] neg_lo:[1,0]
	v_pk_fma_f32 v[82:83], v[10:11], s[40:41], v[34:35] op_sel_hi:[0,1,1]
	v_pk_fma_f32 v[34:35], v[10:11], s[92:93], v[92:93] op_sel_hi:[0,1,1]
	s_mov_b32 s92, 0x3e47c5c2
	v_pk_mul_f32 v[66:67], v[16:17], s[60:61] op_sel_hi:[0,1] neg_lo:[1,0]
	v_pk_fma_f32 v[84:85], v[10:11], s[44:45], v[32:33] op_sel_hi:[0,1,1]
	v_pk_fma_f32 v[60:61], v[10:11], s[82:83], v[52:53] op_sel_hi:[0,1,1]
	s_mov_b32 s82, 0x3f45e403
	s_mov_b32 s93, 0xbf7b14be
	v_pk_mul_f32 v[32:33], v[16:17], s[30:31] op_sel_hi:[0,1] neg_lo:[1,0]
	s_mov_b32 s30, 0x3dc8bd36
	v_pk_mul_f32 v[54:55], v[16:17], s[74:75] op_sel_hi:[0,1] neg_lo:[1,0]
	v_pk_mul_f32 v[62:63], v[16:17], s[54:55] op_sel_hi:[0,1] neg_lo:[1,0]
	s_mov_b32 s83, 0xbf226799
	v_pk_fma_f32 v[52:53], v[10:11], s[86:87], v[66:67] op_sel_hi:[0,1,1]
	s_mov_b32 s31, 0xbf7ec46d
	v_pk_fma_f32 v[66:67], v[10:11], s[92:93], v[32:33] op_sel_hi:[0,1,1]
	v_pk_mul_f32 v[32:33], v[16:17], s[34:35] op_sel_hi:[0,1] neg_lo:[1,0]
	v_pk_fma_f32 v[76:77], v[10:11], s[80:81], v[40:41] op_sel_hi:[0,1,1]
	s_mov_b32 s80, 0x3f61c598
	v_pk_fma_f32 v[58:59], v[10:11], s[82:83], v[54:55] op_sel_hi:[0,1,1]
	v_pk_fma_f32 v[54:55], v[10:11], s[84:85], v[62:63] op_sel_hi:[0,1,1]
	s_mov_b32 s86, 0x3f0e39da
	v_pk_fma_f32 v[62:63], v[10:11], s[30:31], v[32:33] op_sel_hi:[0,1,1]
	v_pk_mul_f32 v[32:33], v[16:17], s[36:37] op_sel_hi:[0,1] neg_lo:[1,0]
	v_pk_mul_f32 v[46:47], v[16:17], s[48:49] op_sel_hi:[0,1] neg_lo:[1,0]
	v_pk_mul_f32 v[86:87], v[16:17], s[66:67] op_sel_hi:[0,1] neg_lo:[1,0]
	s_mov_b32 s81, 0xbef15aea
	s_mov_b32 s87, 0xbf54db31
	v_pk_fma_f32 v[32:33], v[10:11], s[96:97], v[32:33] op_sel_hi:[0,1,1]
	s_mov_b32 s54, 0x3f6c835e
	v_pk_fma_f32 v[64:65], v[10:11], s[80:81], v[46:47] op_sel_hi:[0,1,1]
	v_pk_fma_f32 v[46:47], v[10:11], s[86:87], v[86:87] op_sel_hi:[0,1,1]
	v_pk_mul_f32 v[42:43], v[16:17], s[50:51] op_sel_hi:[0,1] neg_lo:[1,0]
	v_pk_mul_f32 v[88:89], v[16:17], s[68:69] op_sel_hi:[0,1] neg_lo:[1,0]
	s_mov_b32 s55, 0xbec3ef15
	v_pk_fma_f32 v[70:71], v[10:11], s[54:55], v[42:43] op_sel_hi:[0,1,1]
	v_pk_fma_f32 v[42:43], v[10:11], s[88:89], v[88:89] op_sel_hi:[0,1,1]
	s_mov_b32 s88, 0x3ec3ef15
	v_pk_mul_f32 v[90:91], v[16:17], s[56:57] op_sel_hi:[0,1] neg_lo:[1,0]
	s_mov_b32 s89, 0xbf6c835e
	v_pk_fma_f32 v[40:41], v[10:11], s[88:89], v[90:91] op_sel_hi:[0,1,1]
	s_mov_b32 s76, 0x3f7b14be
	s_mov_b32 s77, 0xbe47c5c2
	v_pk_fma_f32 v[80:81], v[10:11], s[76:77], v[36:37] op_sel_hi:[0,1,1]
	v_mov_b32_e32 v36, v169
	v_mov_b32_e32 v15, v171
	s_waitcnt vmcnt(31)
	v_pk_mul_f32 v[86:87], v[32:33], v[94:95] op_sel_hi:[1,0]
	v_pk_mul_f32 v[32:33], v[16:17], s[2:3] op_sel_hi:[0,1] neg_lo:[1,0]
	v_pk_fma_f32 v[32:33], v[10:11], s[0:1], v[32:33] op_sel_hi:[0,1,1]
	s_waitcnt vmcnt(30)
	v_pk_mul_f32 v[88:89], v[32:33], v[96:97] op_sel_hi:[1,0]
	v_pk_mul_f32 v[32:33], v[16:17], s[6:7] op_sel_hi:[0,1] neg_lo:[1,0]
	v_pk_fma_f32 v[32:33], v[10:11], s[4:5], v[32:33] op_sel_hi:[0,1,1]
	s_waitcnt vmcnt(29)
	v_pk_mul_f32 v[90:91], v[32:33], v[98:99] op_sel_hi:[1,0]
	v_pk_mul_f32 v[32:33], v[16:17], s[10:11] op_sel_hi:[0,1] neg_lo:[1,0]
	v_pk_fma_f32 v[32:33], v[10:11], s[8:9], v[32:33] op_sel_hi:[0,1,1]
	s_waitcnt vmcnt(28)
	v_pk_mul_f32 v[92:93], v[32:33], v[100:101] op_sel_hi:[1,0]
	v_pk_mul_f32 v[32:33], v[16:17], s[16:17] op_sel_hi:[0,1] neg_lo:[1,0]
	v_pk_fma_f32 v[32:33], v[10:11], s[12:13], v[32:33] op_sel_hi:[0,1,1]
	s_waitcnt vmcnt(27)
	v_pk_mul_f32 v[94:95], v[32:33], v[102:103] op_sel_hi:[1,0]
	v_pk_mul_f32 v[32:33], v[16:17], s[20:21] op_sel_hi:[0,1] neg_lo:[1,0]
	v_pk_fma_f32 v[32:33], v[10:11], s[18:19], v[32:33] op_sel_hi:[0,1,1]
	s_waitcnt vmcnt(26)
	v_pk_mul_f32 v[96:97], v[32:33], v[104:105] op_sel_hi:[1,0]
	v_pk_mul_f32 v[32:33], v[16:17], s[24:25] op_sel_hi:[0,1] neg_lo:[1,0]
	v_pk_fma_f32 v[32:33], v[10:11], s[22:23], v[32:33] op_sel_hi:[0,1,1]
	s_waitcnt vmcnt(25)
	v_pk_mul_f32 v[98:99], v[32:33], v[106:107] op_sel_hi:[1,0]
	v_pk_mul_f32 v[32:33], v[16:17], s[28:29] op_sel_hi:[0,1] neg_lo:[1,0]
	v_pk_fma_f32 v[32:33], v[10:11], s[26:27], v[32:33] op_sel_hi:[0,1,1]
	s_waitcnt vmcnt(24)
	v_pk_mul_f32 v[100:101], v[32:33], v[108:109] op_sel_hi:[1,0]
	v_pk_mul_f32 v[32:33], v[16:17], s[84:85] op_sel_hi:[0,0] neg_lo:[1,0]
	v_pk_fma_f32 v[32:33], v[10:11], s[38:39], v[32:33] op_sel_hi:[0,0,1] neg_lo:[0,0,1] neg_hi:[0,0,1]
	s_waitcnt vmcnt(23)
	v_pk_mul_f32 v[102:103], v[32:33], v[110:111] op_sel_hi:[1,0]
	v_pk_mul_f32 v[32:33], v[16:17], s[26:27] op_sel_hi:[0,1] neg_lo:[1,0]
	v_pk_fma_f32 v[32:33], v[10:11], s[28:29], v[32:33] op_sel_hi:[0,1,1]
	s_waitcnt vmcnt(22)
	v_pk_mul_f32 v[104:105], v[32:33], v[112:113] op_sel_hi:[1,0]
	v_pk_mul_f32 v[32:33], v[16:17], s[22:23] op_sel_hi:[0,1] neg_lo:[1,0]
	v_pk_fma_f32 v[32:33], v[10:11], s[24:25], v[32:33] op_sel_hi:[0,1,1]
	s_waitcnt vmcnt(21)
	v_pk_mul_f32 v[106:107], v[32:33], v[114:115] op_sel_hi:[1,0]
	v_pk_mul_f32 v[32:33], v[16:17], s[18:19] op_sel_hi:[0,1] neg_lo:[1,0]
	v_pk_fma_f32 v[32:33], v[10:11], s[20:21], v[32:33] op_sel_hi:[0,1,1]
	s_waitcnt vmcnt(20)
	v_pk_mul_f32 v[108:109], v[32:33], v[116:117] op_sel_hi:[1,0]
	v_pk_mul_f32 v[32:33], v[16:17], s[12:13] op_sel_hi:[0,1] neg_lo:[1,0]
	v_pk_fma_f32 v[32:33], v[10:11], s[16:17], v[32:33] op_sel_hi:[0,1,1]
	s_waitcnt vmcnt(19)
	v_pk_mul_f32 v[110:111], v[32:33], v[118:119] op_sel_hi:[1,0]
	v_pk_mul_f32 v[32:33], v[16:17], s[8:9] op_sel_hi:[0,1] neg_lo:[1,0]
	v_pk_fma_f32 v[32:33], v[10:11], s[10:11], v[32:33] op_sel_hi:[0,1,1]
	s_waitcnt vmcnt(18)
	v_pk_mul_f32 v[112:113], v[32:33], v[120:121] op_sel_hi:[1,0]
	v_pk_mul_f32 v[32:33], v[16:17], s[4:5] op_sel_hi:[0,1] neg_lo:[1,0]
	v_pk_mul_f32 v[16:17], v[16:17], s[0:1] op_sel_hi:[0,1] neg_lo:[1,0]
	v_pk_fma_f32 v[16:17], v[10:11], s[2:3], v[16:17] op_sel_hi:[0,1,1]
	v_pk_fma_f32 v[32:33], v[10:11], s[6:7], v[32:33] op_sel_hi:[0,1,1]
	s_waitcnt vmcnt(14)
	v_pk_mul_f32 v[116:117], v[16:17], v[124:125] op_sel_hi:[1,0]
	v_mov_b32_e32 v10, v1
	s_waitcnt vmcnt(5)
	v_pk_fma_f32 v[126:127], v[74:75], v[84:85], v[86:87] op_sel_hi:[0,1,1]
	v_pk_fma_f32 v[74:75], v[74:75], v[84:85], v[86:87] op_sel_hi:[0,1,1] neg_lo:[0,0,1] neg_hi:[0,0,1]
	s_waitcnt vmcnt(4)
	v_pk_fma_f32 v[84:85], v[82:83], v[78:79], v[88:89] op_sel_hi:[1,0,1]
	v_pk_fma_f32 v[78:79], v[82:83], v[78:79], v[88:89] op_sel_hi:[1,0,1] neg_lo:[0,0,1] neg_hi:[0,0,1]
	v_pk_mul_f32 v[114:115], v[32:33], v[122:123] op_sel_hi:[1,0]
	v_mov_b32_e32 v118, v164
	v_mov_b32_e32 v32, v165
	v_mov_b32_e32 v120, v166
	v_mov_b32_e32 v10, v167
	v_mov_b32_e32 v122, v168
	v_mov_b32_e32 v124, v170
	s_nop 0
	v_pk_mul_f32 v[82:83], v[78:79], v[124:125] op_sel:[1,0] op_sel_hi:[0,0] neg_lo:[1,1] neg_hi:[0,1]
	s_nop 0
	v_pk_fma_f32 v[78:79], v[78:79], v[118:119], v[82:83] op_sel_hi:[1,0,1]
	v_pk_fma_f32 v[82:83], v[80:81], v[72:73], v[90:91] op_sel_hi:[1,0,1]
	v_pk_fma_f32 v[72:73], v[80:81], v[72:73], v[90:91] op_sel_hi:[1,0,1] neg_lo:[0,0,1] neg_hi:[0,0,1]
	s_nop 0
	v_pk_mul_f32 v[80:81], v[72:73], v[36:37] op_sel:[1,0] op_sel_hi:[0,0] neg_lo:[1,1] neg_hi:[0,1]
	s_nop 0
	v_pk_fma_f32 v[72:73], v[72:73], v[32:33], v[80:81] op_sel_hi:[1,0,1]
	s_waitcnt vmcnt(3)
	v_pk_fma_f32 v[80:81], v[76:77], v[68:69], v[92:93] op_sel_hi:[1,0,1]
	v_pk_fma_f32 v[68:69], v[76:77], v[68:69], v[92:93] op_sel_hi:[1,0,1] neg_lo:[0,0,1] neg_hi:[0,0,1]
	s_nop 0
	v_pk_mul_f32 v[76:77], v[68:69], v[122:123] op_sel:[1,0] op_sel_hi:[0,0] neg_lo:[1,1] neg_hi:[0,1]
	s_nop 0
	v_pk_fma_f32 v[68:69], v[68:69], v[120:121], v[76:77] op_sel_hi:[1,0,1]
	v_pk_fma_f32 v[76:77], v[70:71], v[56:57], v[94:95] op_sel_hi:[1,0,1]
	v_pk_fma_f32 v[56:57], v[70:71], v[56:57], v[94:95] op_sel_hi:[1,0,1] neg_lo:[0,0,1] neg_hi:[0,0,1]
	s_nop 0
	v_pk_mul_f32 v[70:71], v[56:57], v[10:11] op_sel:[1,0] op_sel_hi:[0,0] neg_lo:[1,1] neg_hi:[0,1]
	s_nop 0
	v_pk_fma_f32 v[56:57], v[56:57], v[10:11], v[70:71] op_sel_hi:[1,0,1]
	v_pk_fma_f32 v[70:71], v[64:65], v[50:51], v[96:97] op_sel_hi:[1,0,1]
	v_pk_fma_f32 v[50:51], v[64:65], v[50:51], v[96:97] op_sel_hi:[1,0,1] neg_lo:[0,0,1] neg_hi:[0,0,1]
	s_nop 0
	v_pk_mul_f32 v[64:65], v[50:51], v[122:123] op_sel_hi:[1,0]
	v_xor_b32_e32 v86, 0x80000000, v51
	v_mov_b32_e32 v87, v50
	v_pk_fma_f32 v[50:51], v[60:61], v[44:45], v[98:99] op_sel_hi:[1,0,1]
	v_pk_fma_f32 v[44:45], v[60:61], v[44:45], v[98:99] op_sel_hi:[1,0,1] neg_lo:[0,0,1] neg_hi:[0,0,1]
	v_pk_fma_f32 v[64:65], v[86:87], v[120:121], v[64:65] op_sel_hi:[1,0,1] neg_lo:[0,1,0] neg_hi:[0,1,0]
	v_pk_mul_f32 v[60:61], v[44:45], v[36:37] op_sel_hi:[1,0]
	v_xor_b32_e32 v86, 0x80000000, v45
	v_mov_b32_e32 v87, v44
	s_waitcnt vmcnt(2)
	v_pk_fma_f32 v[44:45], v[58:59], v[48:49], v[100:101] op_sel_hi:[1,0,1]
	v_pk_fma_f32 v[48:49], v[58:59], v[48:49], v[100:101] op_sel_hi:[1,0,1] neg_lo:[0,0,1] neg_hi:[0,0,1]
	v_pk_fma_f32 v[60:61], v[86:87], v[32:33], v[60:61] op_sel_hi:[1,0,1] neg_lo:[0,1,0] neg_hi:[0,1,0]
	v_pk_mul_f32 v[58:59], v[48:49], v[124:125] op_sel_hi:[1,0]
	s_nop 0
	v_pk_fma_f32 v[48:49], v[48:49], v[118:119], v[58:59] op_sel:[1,0,0] op_sel_hi:[0,0,1] neg_lo:[1,1,0] neg_hi:[0,1,0]
	v_pk_fma_f32 v[58:59], v[54:55], v[38:39], v[102:103] op_sel_hi:[1,0,1]
	v_pk_fma_f32 v[38:39], v[54:55], v[38:39], v[102:103] op_sel_hi:[1,0,1] neg_lo:[0,0,1] neg_hi:[0,0,1]
	s_nop 0
	v_xor_b32_e32 v55, 0x80000000, v38
	v_mov_b32_e32 v54, v39
	v_pk_fma_f32 v[38:39], v[52:53], v[30:31], v[104:105] op_sel_hi:[1,0,1]
	v_pk_fma_f32 v[30:31], v[52:53], v[30:31], v[104:105] op_sel_hi:[1,0,1] neg_lo:[0,0,1] neg_hi:[0,0,1]
	s_nop 0
	v_pk_mul_f32 v[52:53], v[30:31], v[124:125] op_sel_hi:[1,0] neg_lo:[0,1] neg_hi:[0,1]
	v_xor_b32_e32 v86, 0x80000000, v31
	v_mov_b32_e32 v87, v30
	v_pk_fma_f32 v[30:31], v[46:47], v[26:27], v[106:107] op_sel_hi:[1,0,1]
	v_pk_fma_f32 v[26:27], v[46:47], v[26:27], v[106:107] op_sel_hi:[1,0,1] neg_lo:[0,0,1] neg_hi:[0,0,1]
	v_pk_fma_f32 v[52:53], v[86:87], v[118:119], v[52:53] op_sel_hi:[1,0,1] neg_lo:[0,1,0] neg_hi:[0,1,0]
	v_pk_mul_f32 v[46:47], v[26:27], v[36:37] op_sel_hi:[1,0] neg_lo:[0,1] neg_hi:[0,1]
	v_xor_b32_e32 v86, 0x80000000, v27
	v_mov_b32_e32 v87, v26
	s_waitcnt vmcnt(1)
	v_pk_fma_f32 v[26:27], v[42:43], v[28:29], v[108:109] op_sel_hi:[1,0,1]
	v_pk_fma_f32 v[28:29], v[42:43], v[28:29], v[108:109] op_sel_hi:[1,0,1] neg_lo:[0,0,1] neg_hi:[0,0,1]
	v_pk_fma_f32 v[86:87], v[86:87], v[32:33], v[46:47] op_sel_hi:[1,0,1] neg_lo:[0,1,0] neg_hi:[0,1,0]
	v_pk_mul_f32 v[42:43], v[28:29], v[122:123] op_sel_hi:[1,0] neg_lo:[0,1] neg_hi:[0,1]
	v_xor_b32_e32 v46, 0x80000000, v29
	v_mov_b32_e32 v47, v28
	v_pk_fma_f32 v[28:29], v[40:41], v[24:25], v[110:111] op_sel_hi:[1,0,1]
	v_pk_fma_f32 v[24:25], v[40:41], v[24:25], v[110:111] op_sel_hi:[1,0,1] neg_lo:[0,0,1] neg_hi:[0,0,1]
	v_pk_fma_f32 v[42:43], v[46:47], v[120:121], v[42:43] op_sel_hi:[1,0,1] neg_lo:[0,1,0] neg_hi:[0,1,0]
	v_pk_mul_f32 v[40:41], v[24:25], v[10:11] op_sel:[1,0] op_sel_hi:[0,0] neg_lo:[1,1] neg_hi:[0,1]
	s_nop 0
	v_pk_fma_f32 v[88:89], v[24:25], v[10:11], v[40:41] op_sel_hi:[1,0,1] neg_lo:[0,1,0] neg_hi:[0,1,0]
	v_pk_fma_f32 v[24:25], v[34:35], v[22:23], v[112:113] op_sel_hi:[1,0,1]
	v_pk_fma_f32 v[22:23], v[34:35], v[22:23], v[112:113] op_sel_hi:[1,0,1] neg_lo:[0,0,1] neg_hi:[0,0,1]
	v_pk_add_f32 v[40:41], v[84:85], v[38:39]
	v_pk_mul_f32 v[34:35], v[22:23], v[122:123] op_sel:[1,0] op_sel_hi:[0,0] neg_lo:[1,1] neg_hi:[0,1]
	v_pk_add_f32 v[38:39], v[84:85], v[38:39] neg_lo:[0,1] neg_hi:[0,1]
	v_pk_fma_f32 v[90:91], v[22:23], v[120:121], v[34:35] op_sel_hi:[1,0,1] neg_lo:[0,1,0] neg_hi:[0,1,0]
	v_pk_fma_f32 v[22:23], v[66:67], v[20:21], v[114:115] op_sel_hi:[1,0,1]
	v_pk_fma_f32 v[20:21], v[66:67], v[20:21], v[114:115] op_sel_hi:[1,0,1] neg_lo:[0,0,1] neg_hi:[0,0,1]
	s_nop 0
	v_pk_mul_f32 v[34:35], v[20:21], v[36:37] op_sel:[1,0] op_sel_hi:[0,0] neg_lo:[1,1] neg_hi:[0,1]
	v_pk_fma_f32 v[66:67], v[20:21], v[32:33], v[34:35] op_sel_hi:[1,0,1] neg_lo:[0,1,0] neg_hi:[0,1,0]
	s_waitcnt vmcnt(0)
	v_pk_fma_f32 v[20:21], v[62:63], v[18:19], v[116:117] op_sel_hi:[1,0,1]
	v_pk_fma_f32 v[18:19], v[62:63], v[18:19], v[116:117] op_sel_hi:[1,0,1] neg_lo:[0,0,1] neg_hi:[0,0,1]
	v_pk_mul_f32 v[46:47], v[38:39], v[36:37] op_sel:[1,0] op_sel_hi:[0,0] neg_lo:[1,1] neg_hi:[0,1]
	v_pk_mul_f32 v[34:35], v[18:19], v[124:125] op_sel:[1,0] op_sel_hi:[0,0] neg_lo:[1,1] neg_hi:[0,1]
	v_pk_fma_f32 v[38:39], v[38:39], v[32:33], v[46:47] op_sel_hi:[1,0,1]
	v_pk_add_f32 v[46:47], v[82:83], v[30:31]
	v_pk_add_f32 v[30:31], v[82:83], v[30:31] neg_lo:[0,1] neg_hi:[0,1]
	v_pk_fma_f32 v[62:63], v[18:19], v[118:119], v[34:35] op_sel_hi:[1,0,1] neg_lo:[0,1,0] neg_hi:[0,1,0]
	v_pk_add_f32 v[18:19], v[126:127], v[58:59]
	v_pk_add_f32 v[34:35], v[126:127], v[58:59] neg_lo:[0,1] neg_hi:[0,1]
	v_pk_mul_f32 v[58:59], v[30:31], v[10:11] op_sel:[1,0] op_sel_hi:[0,0] neg_lo:[1,1] neg_hi:[0,1]
	s_nop 0
	v_pk_fma_f32 v[58:59], v[30:31], v[10:11], v[58:59] op_sel_hi:[1,0,1]
	v_pk_add_f32 v[30:31], v[80:81], v[26:27]
	v_pk_add_f32 v[26:27], v[80:81], v[26:27] neg_lo:[0,1] neg_hi:[0,1]
	s_nop 0
	v_pk_mul_f32 v[80:81], v[26:27], v[36:37] op_sel_hi:[1,0]
	v_xor_b32_e32 v82, 0x80000000, v27
	v_mov_b32_e32 v83, v26
	v_pk_add_f32 v[26:27], v[76:77], v[28:29]
	v_pk_add_f32 v[28:29], v[76:77], v[28:29] neg_lo:[0,1] neg_hi:[0,1]
	v_pk_fma_f32 v[80:81], v[82:83], v[32:33], v[80:81] op_sel_hi:[1,0,1] neg_lo:[0,1,0] neg_hi:[0,1,0]
	v_xor_b32_e32 v77, 0x80000000, v28
	v_mov_b32_e32 v76, v29
	v_pk_add_f32 v[28:29], v[70:71], v[24:25]
	v_pk_add_f32 v[24:25], v[70:71], v[24:25] neg_lo:[0,1] neg_hi:[0,1]
	s_nop 0
	v_pk_mul_f32 v[70:71], v[24:25], v[36:37] op_sel_hi:[1,0] neg_lo:[0,1] neg_hi:[0,1]
	s_nop 0
	v_pk_fma_f32 v[24:25], v[24:25], v[32:33], v[70:71] op_sel:[1,0,0] op_sel_hi:[0,0,1] neg_lo:[1,1,0] neg_hi:[0,1,0]
	v_pk_add_f32 v[70:71], v[50:51], v[22:23]
	v_pk_add_f32 v[22:23], v[50:51], v[22:23] neg_lo:[0,1] neg_hi:[0,1]
	s_nop 0
	v_pk_mul_f32 v[50:51], v[22:23], v[10:11] op_sel:[1,0] op_sel_hi:[0,0] neg_lo:[1,1] neg_hi:[0,1]
	s_nop 0
	v_pk_fma_f32 v[50:51], v[22:23], v[10:11], v[50:51] op_sel_hi:[1,0,1] neg_lo:[0,1,0] neg_hi:[0,1,0]
	v_pk_add_f32 v[22:23], v[44:45], v[20:21]
	v_pk_add_f32 v[20:21], v[44:45], v[20:21] neg_lo:[0,1] neg_hi:[0,1]
	s_nop 0
	v_pk_mul_f32 v[44:45], v[20:21], v[36:37] op_sel:[1,0] op_sel_hi:[0,0] neg_lo:[1,1] neg_hi:[0,1]
	s_nop 0
	v_pk_fma_f32 v[20:21], v[20:21], v[32:33], v[44:45] op_sel_hi:[1,0,1] neg_lo:[0,1,0] neg_hi:[0,1,0]
	v_pk_add_f32 v[44:45], v[18:19], v[26:27]
	v_pk_add_f32 v[18:19], v[18:19], v[26:27] neg_lo:[0,1] neg_hi:[0,1]
	v_pk_add_f32 v[26:27], v[40:41], v[28:29]
	v_pk_add_f32 v[28:29], v[40:41], v[28:29] neg_lo:[0,1] neg_hi:[0,1]
	s_nop 0
	v_pk_mul_f32 v[40:41], v[28:29], v[10:11] op_sel:[1,0] op_sel_hi:[0,0] neg_lo:[1,1] neg_hi:[0,1]
	s_nop 0
	v_pk_fma_f32 v[28:29], v[28:29], v[10:11], v[40:41] op_sel_hi:[1,0,1]
	v_pk_add_f32 v[40:41], v[46:47], v[70:71]
	v_pk_add_f32 v[46:47], v[46:47], v[70:71] neg_lo:[0,1] neg_hi:[0,1]
	s_nop 0
	v_xor_b32_e32 v71, 0x80000000, v46
	v_mov_b32_e32 v70, v47
	v_pk_add_f32 v[46:47], v[30:31], v[22:23]
	v_pk_add_f32 v[22:23], v[30:31], v[22:23] neg_lo:[0,1] neg_hi:[0,1]
	s_nop 0
	v_pk_mul_f32 v[30:31], v[22:23], v[10:11] op_sel:[1,0] op_sel_hi:[0,0] neg_lo:[1,1] neg_hi:[0,1]
	s_nop 0
	v_pk_fma_f32 v[82:83], v[22:23], v[10:11], v[30:31] op_sel_hi:[1,0,1] neg_lo:[0,1,0] neg_hi:[0,1,0]
	v_pk_add_f32 v[30:31], v[26:27], v[46:47]
	v_pk_add_f32 v[26:27], v[26:27], v[46:47] neg_lo:[0,1] neg_hi:[0,1]
	v_pk_add_f32 v[22:23], v[44:45], v[40:41]
	v_pk_add_f32 v[40:41], v[44:45], v[40:41] neg_lo:[0,1] neg_hi:[0,1]
	v_pk_add_f32 v[84:85], v[22:23], v[30:31]
	v_pk_add_f32 v[30:31], v[22:23], v[30:31] neg_lo:[0,1] neg_hi:[0,1]
	v_pk_add_f32 v[46:47], v[40:41], v[26:27] op_sel:[0,1] op_sel_hi:[1,0] neg_hi:[0,1]
	v_pk_add_f32 v[22:23], v[40:41], v[26:27] op_sel:[0,1] op_sel_hi:[1,0] neg_lo:[0,1]
	v_pk_add_f32 v[40:41], v[28:29], v[82:83]
	v_pk_add_f32 v[28:29], v[28:29], v[82:83] neg_lo:[0,1] neg_hi:[0,1]
	v_pk_add_f32 v[26:27], v[18:19], v[70:71]
	v_pk_add_f32 v[18:19], v[18:19], v[70:71] neg_lo:[0,1] neg_hi:[0,1]
	v_pk_add_f32 v[70:71], v[26:27], v[40:41]
	v_pk_add_f32 v[26:27], v[26:27], v[40:41] neg_lo:[0,1] neg_hi:[0,1]
	v_pk_add_f32 v[40:41], v[18:19], v[28:29] op_sel:[0,1] op_sel_hi:[1,0] neg_hi:[0,1]
	v_pk_add_f32 v[18:19], v[18:19], v[28:29] op_sel:[0,1] op_sel_hi:[1,0] neg_lo:[0,1]
	v_pk_add_f32 v[28:29], v[34:35], v[76:77]
	v_pk_add_f32 v[44:45], v[34:35], v[76:77] neg_lo:[0,1] neg_hi:[0,1]
	v_pk_add_f32 v[34:35], v[38:39], v[24:25]
	v_pk_add_f32 v[24:25], v[38:39], v[24:25] neg_lo:[0,1] neg_hi:[0,1]
	s_nop 0
	v_pk_mul_f32 v[38:39], v[10:11], v[24:25] op_sel:[0,1] op_sel_hi:[0,0] neg_lo:[1,1] neg_hi:[1,0]
	v_pk_fma_f32 v[38:39], v[10:11], v[24:25], v[38:39] op_sel_hi:[0,1,1]
	v_pk_add_f32 v[24:25], v[58:59], v[50:51]
	v_pk_add_f32 v[50:51], v[58:59], v[50:51] neg_lo:[0,1] neg_hi:[0,1]
	s_nop 0
	v_xor_b32_e32 v59, 0x80000000, v50
	v_mov_b32_e32 v58, v51
	v_pk_add_f32 v[50:51], v[80:81], v[20:21]
	v_pk_add_f32 v[20:21], v[80:81], v[20:21] neg_lo:[0,1] neg_hi:[0,1]
	s_nop 0
	v_pk_mul_f32 v[76:77], v[10:11], v[20:21] op_sel:[0,1] op_sel_hi:[0,0] neg_lo:[1,1] neg_hi:[1,0]
	v_pk_fma_f32 v[20:21], v[10:11], v[20:21], v[76:77] op_sel_hi:[0,1,1] neg_lo:[1,0,0] neg_hi:[1,0,0]
	v_pk_add_f32 v[76:77], v[28:29], v[24:25]
	v_pk_add_f32 v[24:25], v[28:29], v[24:25] neg_lo:[0,1] neg_hi:[0,1]
	v_pk_add_f32 v[28:29], v[34:35], v[50:51]
	v_pk_add_f32 v[34:35], v[34:35], v[50:51] neg_lo:[0,1] neg_hi:[0,1]
	v_pk_add_f32 v[82:83], v[76:77], v[28:29]
	v_xor_b32_e32 v81, 0x80000000, v34
	v_mov_b32_e32 v80, v35
	v_pk_add_f32 v[34:35], v[76:77], v[28:29] neg_lo:[0,1] neg_hi:[0,1]
	v_pk_add_f32 v[28:29], v[44:45], v[58:59]
	v_pk_add_f32 v[58:59], v[44:45], v[58:59] neg_lo:[0,1] neg_hi:[0,1]
	v_pk_add_f32 v[44:45], v[38:39], v[20:21]
	v_pk_add_f32 v[20:21], v[38:39], v[20:21] neg_lo:[0,1] neg_hi:[0,1]
	v_pk_add_f32 v[76:77], v[28:29], v[44:45]
	v_pk_add_f32 v[28:29], v[28:29], v[44:45] neg_lo:[0,1] neg_hi:[0,1]
	v_pk_add_f32 v[44:45], v[58:59], v[20:21] op_sel:[0,1] op_sel_hi:[1,0] neg_hi:[0,1]
	v_pk_add_f32 v[20:21], v[58:59], v[20:21] op_sel:[0,1] op_sel_hi:[1,0] neg_lo:[0,1]
	v_pk_add_f32 v[38:39], v[74:75], v[54:55]
	v_pk_add_f32 v[58:59], v[74:75], v[54:55] neg_lo:[0,1] neg_hi:[0,1]
	v_pk_add_f32 v[54:55], v[78:79], v[52:53]
	v_pk_add_f32 v[52:53], v[78:79], v[52:53] neg_lo:[0,1] neg_hi:[0,1]
	v_pk_add_f32 v[50:51], v[24:25], v[80:81]
	v_pk_mul_f32 v[74:75], v[36:37], v[52:53] op_sel:[0,1] op_sel_hi:[0,0] neg_lo:[1,1] neg_hi:[1,0]
	v_pk_fma_f32 v[52:53], v[32:33], v[52:53], v[74:75] op_sel_hi:[0,1,1]
	v_pk_add_f32 v[74:75], v[72:73], v[86:87]
	v_pk_add_f32 v[72:73], v[72:73], v[86:87] neg_lo:[0,1] neg_hi:[0,1]
	v_pk_add_f32 v[24:25], v[24:25], v[80:81] neg_lo:[0,1] neg_hi:[0,1]
	v_pk_mul_f32 v[78:79], v[10:11], v[72:73] op_sel:[0,1] op_sel_hi:[0,0] neg_lo:[1,1] neg_hi:[1,0]
	v_pk_fma_f32 v[72:73], v[10:11], v[72:73], v[78:79] op_sel_hi:[0,1,1]
	v_pk_add_f32 v[78:79], v[68:69], v[42:43]
	v_pk_add_f32 v[42:43], v[68:69], v[42:43] neg_lo:[0,1] neg_hi:[0,1]
	s_nop 0
	v_pk_mul_f32 v[68:69], v[32:33], v[42:43] op_sel:[0,1] op_sel_hi:[0,0] neg_lo:[1,1] neg_hi:[1,0]
	v_pk_fma_f32 v[42:43], v[36:37], v[42:43], v[68:69] op_sel_hi:[0,1,1]
	v_pk_add_f32 v[68:69], v[56:57], v[88:89]
	v_pk_add_f32 v[56:57], v[56:57], v[88:89] neg_lo:[0,1] neg_hi:[0,1]
	s_nop 0
	v_xor_b32_e32 v81, 0x80000000, v56
	v_mov_b32_e32 v80, v57
	v_pk_add_f32 v[56:57], v[64:65], v[90:91]
	v_pk_add_f32 v[64:65], v[64:65], v[90:91] neg_lo:[0,1] neg_hi:[0,1]
	s_nop 0
	v_pk_mul_f32 v[86:87], v[32:33], v[64:65] op_sel:[0,1] op_sel_hi:[0,0] neg_lo:[1,1] neg_hi:[1,0]
	v_pk_fma_f32 v[64:65], v[36:37], v[64:65], v[86:87] op_sel_hi:[0,1,1] neg_lo:[1,0,0] neg_hi:[1,0,0]
	v_pk_add_f32 v[86:87], v[60:61], v[66:67]
	v_pk_add_f32 v[60:61], v[60:61], v[66:67] neg_lo:[0,1] neg_hi:[0,1]
	s_nop 0
	v_pk_mul_f32 v[66:67], v[10:11], v[60:61] op_sel:[0,1] op_sel_hi:[0,0] neg_lo:[1,1] neg_hi:[1,0]
	v_pk_fma_f32 v[60:61], v[10:11], v[60:61], v[66:67] op_sel_hi:[0,1,1] neg_lo:[1,0,0] neg_hi:[1,0,0]
	v_pk_add_f32 v[66:67], v[48:49], v[62:63]
	v_pk_add_f32 v[48:49], v[48:49], v[62:63] neg_lo:[0,1] neg_hi:[0,1]
	s_nop 0
	v_pk_mul_f32 v[36:37], v[36:37], v[48:49] op_sel:[0,1] op_sel_hi:[0,0] neg_lo:[1,1] neg_hi:[1,0]
	v_pk_fma_f32 v[36:37], v[32:33], v[48:49], v[36:37] op_sel_hi:[0,1,1] neg_lo:[1,0,0] neg_hi:[1,0,0]
	v_pk_add_f32 v[32:33], v[38:39], v[68:69]
	v_pk_add_f32 v[48:49], v[38:39], v[68:69] neg_lo:[0,1] neg_hi:[0,1]
	v_pk_add_f32 v[38:39], v[56:57], v[54:55]
	v_pk_add_f32 v[54:55], v[54:55], v[56:57] neg_lo:[0,1] neg_hi:[0,1]
	v_pk_add_f32 v[62:63], v[74:75], v[86:87] neg_lo:[0,1] neg_hi:[0,1]
	v_pk_mul_f32 v[56:57], v[10:11], v[54:55] op_sel:[0,1] op_sel_hi:[0,0] neg_lo:[1,1] neg_hi:[1,0]
	v_xor_b32_e32 v69, 0x80000000, v62
	v_mov_b32_e32 v68, v63
	v_pk_add_f32 v[62:63], v[78:79], v[66:67]
	v_pk_add_f32 v[66:67], v[78:79], v[66:67] neg_lo:[0,1] neg_hi:[0,1]
	v_pk_fma_f32 v[56:57], v[10:11], v[54:55], v[56:57] op_sel_hi:[0,1,1]
	v_pk_add_f32 v[54:55], v[74:75], v[86:87]
	v_pk_mul_f32 v[74:75], v[10:11], v[66:67] op_sel:[0,1] op_sel_hi:[0,0] neg_lo:[1,1] neg_hi:[1,0]
	v_pk_fma_f32 v[66:67], v[10:11], v[66:67], v[74:75] op_sel_hi:[0,1,1] neg_lo:[1,0,0] neg_hi:[1,0,0]
	v_pk_add_f32 v[74:75], v[32:33], v[54:55]
	v_pk_add_f32 v[32:33], v[32:33], v[54:55] neg_lo:[0,1] neg_hi:[0,1]
	v_pk_add_f32 v[54:55], v[38:39], v[62:63]
	v_pk_add_f32 v[38:39], v[38:39], v[62:63] neg_lo:[0,1] neg_hi:[0,1]
	v_pk_add_f32 v[78:79], v[74:75], v[54:55]
	v_pk_add_f32 v[54:55], v[74:75], v[54:55] neg_lo:[0,1] neg_hi:[0,1]
	v_pk_add_f32 v[74:75], v[32:33], v[38:39] op_sel:[0,1] op_sel_hi:[1,0] neg_hi:[0,1]
	v_pk_add_f32 v[38:39], v[32:33], v[38:39] op_sel:[0,1] op_sel_hi:[1,0] neg_lo:[0,1]
	v_pk_add_f32 v[32:33], v[48:49], v[68:69]
	v_pk_add_f32 v[62:63], v[48:49], v[68:69] neg_lo:[0,1] neg_hi:[0,1]
	v_pk_add_f32 v[48:49], v[56:57], v[66:67]
	v_pk_add_f32 v[56:57], v[56:57], v[66:67] neg_lo:[0,1] neg_hi:[0,1]
	s_nop 0
	v_xor_b32_e32 v67, 0x80000000, v56
	v_mov_b32_e32 v66, v57
	v_pk_add_f32 v[56:57], v[32:33], v[48:49]
	v_pk_add_f32 v[48:49], v[32:33], v[48:49] neg_lo:[0,1] neg_hi:[0,1]
	v_pk_add_f32 v[68:69], v[62:63], v[66:67]
	v_pk_add_f32 v[32:33], v[62:63], v[66:67] neg_lo:[0,1] neg_hi:[0,1]
	v_pk_add_f32 v[66:67], v[64:65], v[52:53]
	v_pk_add_f32 v[52:53], v[52:53], v[64:65] neg_lo:[0,1] neg_hi:[0,1]
	v_pk_add_f32 v[62:63], v[58:59], v[80:81]
	v_pk_mul_f32 v[64:65], v[10:11], v[52:53] op_sel:[0,1] op_sel_hi:[0,0] neg_lo:[1,1] neg_hi:[1,0]
	v_pk_fma_f32 v[52:53], v[10:11], v[52:53], v[64:65] op_sel_hi:[0,1,1]
	v_pk_add_f32 v[64:65], v[72:73], v[60:61]
	v_pk_add_f32 v[60:61], v[72:73], v[60:61] neg_lo:[0,1] neg_hi:[0,1]
	v_pk_add_f32 v[58:59], v[58:59], v[80:81] neg_lo:[0,1] neg_hi:[0,1]
	v_xor_b32_e32 v73, 0x80000000, v60
	v_mov_b32_e32 v72, v61
	v_pk_add_f32 v[60:61], v[42:43], v[36:37]
	v_pk_add_f32 v[36:37], v[42:43], v[36:37] neg_lo:[0,1] neg_hi:[0,1]
	s_nop 0
	v_pk_mul_f32 v[42:43], v[10:11], v[36:37] op_sel:[0,1] op_sel_hi:[0,0] neg_lo:[1,1] neg_hi:[1,0]
	v_pk_fma_f32 v[36:37], v[10:11], v[36:37], v[42:43] op_sel_hi:[0,1,1] neg_lo:[1,0,0] neg_hi:[1,0,0]
	v_pk_add_f32 v[42:43], v[62:63], v[64:65]
	v_pk_add_f32 v[62:63], v[62:63], v[64:65] neg_lo:[0,1] neg_hi:[0,1]
	v_pk_add_f32 v[64:65], v[66:67], v[60:61]
	v_pk_add_f32 v[60:61], v[66:67], v[60:61] neg_lo:[0,1] neg_hi:[0,1]
	v_lshl_add_u32 v10, v13, 3, 0
	v_xor_b32_e32 v67, 0x80000000, v60
	v_mov_b32_e32 v66, v61
	v_pk_add_f32 v[60:61], v[42:43], v[64:65]
	v_pk_add_f32 v[64:65], v[42:43], v[64:65] neg_lo:[0,1] neg_hi:[0,1]
	v_pk_add_f32 v[80:81], v[62:63], v[66:67]
	v_pk_add_f32 v[42:43], v[62:63], v[66:67] neg_lo:[0,1] neg_hi:[0,1]
	v_pk_add_f32 v[66:67], v[52:53], v[36:37]
	v_pk_add_f32 v[36:37], v[52:53], v[36:37] neg_lo:[0,1] neg_hi:[0,1]
	v_pk_add_f32 v[62:63], v[58:59], v[72:73]
	v_pk_add_f32 v[58:59], v[58:59], v[72:73] neg_lo:[0,1] neg_hi:[0,1]
	v_pk_add_f32 v[86:87], v[62:63], v[66:67]
	v_pk_add_f32 v[52:53], v[62:63], v[66:67] neg_lo:[0,1] neg_hi:[0,1]
	v_pk_add_f32 v[62:63], v[58:59], v[36:37] op_sel:[0,1] op_sel_hi:[1,0] neg_hi:[0,1]
	v_pk_add_f32 v[36:37], v[58:59], v[36:37] op_sel:[0,1] op_sel_hi:[1,0] neg_lo:[0,1]
	v_pk_mul_f32 v[58:59], v[84:85], s[14:15] op_sel:[1,0] neg_lo:[1,0]
	s_nop 0
	v_pk_fma_f32 v[58:59], v[84:85], s[94:95], v[58:59] op_sel_hi:[0,1,1]
	ds_write_b64 v10, v[58:59]
	v_pk_fma_f32 v[58:59], v[178:179], s[90:91], v[178:179] op_sel:[1,0,0] op_sel_hi:[0,1,1]
	v_pk_mul_f32 v[66:67], v[58:59], v[78:79] op_sel:[1,1] op_sel_hi:[0,1] neg_lo:[0,1]
	v_pk_fma_f32 v[66:67], v[58:59], v[78:79], v[66:67] op_sel_hi:[1,0,1]
	ds_write_b64 v10, v[66:67] offset:4224
	v_pk_mul_f32 v[66:67], v[178:179], v[58:59] op_sel:[1,1] op_sel_hi:[0,1] neg_lo:[0,1]
	v_pk_fma_f32 v[58:59], v[178:179], v[58:59], v[66:67] op_sel_hi:[1,0,1]
	s_nop 0
	v_pk_mul_f32 v[66:67], v[58:59], v[82:83] op_sel:[1,1] op_sel_hi:[0,1] neg_lo:[0,1]
	v_pk_fma_f32 v[66:67], v[58:59], v[82:83], v[66:67] op_sel_hi:[1,0,1]
	ds_write_b64 v10, v[66:67] offset:8448
	v_pk_mul_f32 v[66:67], v[178:179], v[58:59] op_sel:[1,1] op_sel_hi:[0,1] neg_lo:[0,1]
	v_pk_fma_f32 v[58:59], v[178:179], v[58:59], v[66:67] op_sel_hi:[1,0,1]
	s_nop 0
	v_pk_mul_f32 v[66:67], v[58:59], v[60:61] op_sel:[1,1] op_sel_hi:[0,1] neg_lo:[0,1]
	v_pk_fma_f32 v[60:61], v[58:59], v[60:61], v[66:67] op_sel_hi:[1,0,1]
	ds_write_b64 v10, v[60:61] offset:12672
	v_pk_mul_f32 v[60:61], v[178:179], v[58:59] op_sel:[1,1] op_sel_hi:[0,1] neg_lo:[0,1]
	v_pk_fma_f32 v[58:59], v[178:179], v[58:59], v[60:61] op_sel_hi:[1,0,1]
	s_nop 0
	v_pk_mul_f32 v[60:61], v[70:71], v[58:59] op_sel:[1,1] op_sel_hi:[1,0] neg_lo:[1,0]
	s_nop 0
	v_pk_fma_f32 v[60:61], v[70:71], v[58:59], v[60:61] op_sel_hi:[0,1,1]
	ds_write_b64 v10, v[60:61] offset:16896
	v_pk_mul_f32 v[60:61], v[178:179], v[58:59] op_sel:[1,1] op_sel_hi:[0,1] neg_lo:[0,1]
	v_pk_fma_f32 v[58:59], v[178:179], v[58:59], v[60:61] op_sel_hi:[1,0,1]
	s_nop 0
	v_pk_mul_f32 v[60:61], v[58:59], v[56:57] op_sel:[1,1] op_sel_hi:[0,1] neg_lo:[0,1]
	v_pk_fma_f32 v[56:57], v[58:59], v[56:57], v[60:61] op_sel_hi:[1,0,1]
	ds_write_b64 v10, v[56:57] offset:21120
	v_pk_mul_f32 v[56:57], v[178:179], v[58:59] op_sel:[1,1] op_sel_hi:[0,1] neg_lo:[0,1]
	v_pk_fma_f32 v[56:57], v[178:179], v[58:59], v[56:57] op_sel_hi:[1,0,1]
	s_nop 0
	v_pk_mul_f32 v[58:59], v[76:77], v[56:57] op_sel:[1,1] op_sel_hi:[1,0] neg_lo:[1,0]
	s_nop 0
	v_pk_fma_f32 v[58:59], v[76:77], v[56:57], v[58:59] op_sel_hi:[0,1,1]
	ds_write_b64 v10, v[58:59] offset:25344
	v_pk_mul_f32 v[58:59], v[178:179], v[56:57] op_sel:[1,1] op_sel_hi:[0,1] neg_lo:[0,1]
	v_pk_fma_f32 v[56:57], v[178:179], v[56:57], v[58:59] op_sel_hi:[1,0,1]
	s_nop 0
	v_pk_mul_f32 v[58:59], v[86:87], v[56:57] op_sel:[1,1] op_sel_hi:[1,0] neg_lo:[1,0]
	s_nop 0
	v_pk_fma_f32 v[58:59], v[86:87], v[56:57], v[58:59] op_sel_hi:[0,1,1]
	ds_write_b64 v10, v[58:59] offset:29568
	v_pk_mul_f32 v[58:59], v[178:179], v[56:57] op_sel:[1,1] op_sel_hi:[0,1] neg_lo:[0,1]
	v_pk_fma_f32 v[56:57], v[178:179], v[56:57], v[58:59] op_sel_hi:[1,0,1]
	s_nop 0
	v_pk_mul_f32 v[58:59], v[46:47], v[56:57] op_sel:[1,1] op_sel_hi:[1,0] neg_lo:[1,0]
	s_nop 0
	v_pk_fma_f32 v[46:47], v[46:47], v[56:57], v[58:59] op_sel_hi:[0,1,1]
	ds_write_b64 v10, v[46:47] offset:33792
	v_pk_mul_f32 v[46:47], v[178:179], v[56:57] op_sel:[1,1] op_sel_hi:[0,1] neg_lo:[0,1]
	v_pk_fma_f32 v[46:47], v[178:179], v[56:57], v[46:47] op_sel_hi:[1,0,1]
	s_nop 0
	v_pk_mul_f32 v[56:57], v[74:75], v[46:47] op_sel:[1,1] op_sel_hi:[1,0] neg_lo:[1,0]
	s_nop 0
	v_pk_fma_f32 v[56:57], v[74:75], v[46:47], v[56:57] op_sel_hi:[0,1,1]
	ds_write_b64 v10, v[56:57] offset:38016
	v_pk_mul_f32 v[56:57], v[178:179], v[46:47] op_sel:[1,1] op_sel_hi:[0,1] neg_lo:[0,1]
	v_pk_fma_f32 v[46:47], v[178:179], v[46:47], v[56:57] op_sel_hi:[1,0,1]
	s_nop 0
	v_pk_mul_f32 v[56:57], v[50:51], v[46:47] op_sel:[1,1] op_sel_hi:[1,0] neg_lo:[1,0]
	s_nop 0
	v_pk_fma_f32 v[50:51], v[50:51], v[46:47], v[56:57] op_sel_hi:[0,1,1]
	ds_write_b64 v10, v[50:51] offset:42240
	v_pk_mul_f32 v[50:51], v[178:179], v[46:47] op_sel:[1,1] op_sel_hi:[0,1] neg_lo:[0,1]
	v_pk_fma_f32 v[46:47], v[178:179], v[46:47], v[50:51] op_sel_hi:[1,0,1]
	s_nop 0
	v_pk_mul_f32 v[50:51], v[80:81], v[46:47] op_sel:[1,1] op_sel_hi:[1,0] neg_lo:[1,0]
	s_nop 0
	v_pk_fma_f32 v[50:51], v[80:81], v[46:47], v[50:51] op_sel_hi:[0,1,1]
	ds_write_b64 v10, v[50:51] offset:46464
	v_pk_mul_f32 v[50:51], v[178:179], v[46:47] op_sel:[1,1] op_sel_hi:[0,1] neg_lo:[0,1]
	v_pk_fma_f32 v[46:47], v[178:179], v[46:47], v[50:51] op_sel_hi:[1,0,1]
	s_nop 0
	v_pk_mul_f32 v[50:51], v[40:41], v[46:47] op_sel:[1,1] op_sel_hi:[1,0] neg_lo:[1,0]
	s_nop 0
	v_pk_fma_f32 v[40:41], v[40:41], v[46:47], v[50:51] op_sel_hi:[0,1,1]
	ds_write_b64 v10, v[40:41] offset:50688
	v_pk_mul_f32 v[40:41], v[178:179], v[46:47] op_sel:[1,1] op_sel_hi:[0,1] neg_lo:[0,1]
	v_pk_fma_f32 v[40:41], v[178:179], v[46:47], v[40:41] op_sel_hi:[1,0,1]
	s_nop 0
	v_pk_mul_f32 v[46:47], v[68:69], v[40:41] op_sel:[1,1] op_sel_hi:[1,0] neg_lo:[1,0]
	s_nop 0
	v_pk_fma_f32 v[46:47], v[68:69], v[40:41], v[46:47] op_sel_hi:[0,1,1]
	ds_write_b64 v10, v[46:47] offset:54912
	v_pk_mul_f32 v[46:47], v[178:179], v[40:41] op_sel:[1,1] op_sel_hi:[0,1] neg_lo:[0,1]
	v_pk_fma_f32 v[40:41], v[178:179], v[40:41], v[46:47] op_sel_hi:[1,0,1]
	s_nop 0
	v_pk_mul_f32 v[46:47], v[44:45], v[40:41] op_sel:[1,1] op_sel_hi:[1,0] neg_lo:[1,0]
	s_nop 0
	v_pk_fma_f32 v[44:45], v[44:45], v[40:41], v[46:47] op_sel_hi:[0,1,1]
	ds_write_b64 v10, v[44:45] offset:59136
	v_pk_mul_f32 v[44:45], v[178:179], v[40:41] op_sel:[1,1] op_sel_hi:[0,1] neg_lo:[0,1]
	v_pk_fma_f32 v[40:41], v[178:179], v[40:41], v[44:45] op_sel_hi:[1,0,1]
	s_nop 0
	v_pk_mul_f32 v[44:45], v[62:63], v[40:41] op_sel:[1,1] op_sel_hi:[1,0] neg_lo:[1,0]
	s_nop 0
	v_pk_fma_f32 v[44:45], v[62:63], v[40:41], v[44:45] op_sel_hi:[0,1,1]
	ds_write_b64 v10, v[44:45] offset:63360
	v_pk_mul_f32 v[44:45], v[178:179], v[40:41] op_sel:[1,1] op_sel_hi:[0,1] neg_lo:[0,1]
	v_pk_fma_f32 v[40:41], v[178:179], v[40:41], v[44:45] op_sel_hi:[1,0,1]
	s_nop 0
	v_pk_mul_f32 v[44:45], v[30:31], v[40:41] op_sel:[1,1] op_sel_hi:[1,0] neg_lo:[1,0]
	v_add_u32_e32 v13, 0x10800, v10
	v_pk_fma_f32 v[30:31], v[30:31], v[40:41], v[44:45] op_sel_hi:[0,1,1]
	ds_write_b64 v13, v[30:31]
	v_pk_mul_f32 v[30:31], v[178:179], v[40:41] op_sel:[1,1] op_sel_hi:[0,1] neg_lo:[0,1]
	v_pk_fma_f32 v[30:31], v[178:179], v[40:41], v[30:31] op_sel_hi:[1,0,1]
	s_nop 0
	v_pk_mul_f32 v[40:41], v[54:55], v[30:31] op_sel:[1,1] op_sel_hi:[1,0] neg_lo:[1,0]
	v_add_u32_e32 v13, 0x11880, v10
	v_pk_fma_f32 v[40:41], v[54:55], v[30:31], v[40:41] op_sel_hi:[0,1,1]
	ds_write_b64 v13, v[40:41]
	v_pk_mul_f32 v[40:41], v[178:179], v[30:31] op_sel:[1,1] op_sel_hi:[0,1] neg_lo:[0,1]
	v_pk_fma_f32 v[30:31], v[178:179], v[30:31], v[40:41] op_sel_hi:[1,0,1]
	s_nop 0
	v_pk_mul_f32 v[40:41], v[34:35], v[30:31] op_sel:[1,1] op_sel_hi:[1,0] neg_lo:[1,0]
	v_add_u32_e32 v13, 0x12900, v10
	v_pk_fma_f32 v[34:35], v[34:35], v[30:31], v[40:41] op_sel_hi:[0,1,1]
	ds_write_b64 v13, v[34:35]
	v_pk_mul_f32 v[34:35], v[178:179], v[30:31] op_sel:[1,1] op_sel_hi:[0,1] neg_lo:[0,1]
	v_pk_fma_f32 v[30:31], v[178:179], v[30:31], v[34:35] op_sel_hi:[1,0,1]
	s_nop 0
	v_pk_mul_f32 v[34:35], v[64:65], v[30:31] op_sel:[1,1] op_sel_hi:[1,0] neg_lo:[1,0]
	v_add_u32_e32 v13, 0x13980, v10
	v_pk_fma_f32 v[34:35], v[64:65], v[30:31], v[34:35] op_sel_hi:[0,1,1]
	ds_write_b64 v13, v[34:35]
	v_pk_mul_f32 v[34:35], v[178:179], v[30:31] op_sel:[1,1] op_sel_hi:[0,1] neg_lo:[0,1]
	v_pk_fma_f32 v[30:31], v[178:179], v[30:31], v[34:35] op_sel_hi:[1,0,1]
	s_nop 0
	v_pk_mul_f32 v[34:35], v[26:27], v[30:31] op_sel:[1,1] op_sel_hi:[1,0] neg_lo:[1,0]
	v_add_u32_e32 v13, 0x14a00, v10
	v_pk_fma_f32 v[26:27], v[26:27], v[30:31], v[34:35] op_sel_hi:[0,1,1]
	ds_write_b64 v13, v[26:27]
	v_pk_mul_f32 v[26:27], v[178:179], v[30:31] op_sel:[1,1] op_sel_hi:[0,1] neg_lo:[0,1]
	v_pk_fma_f32 v[26:27], v[178:179], v[30:31], v[26:27] op_sel_hi:[1,0,1]
	s_nop 0
	v_pk_mul_f32 v[30:31], v[48:49], v[26:27] op_sel:[1,1] op_sel_hi:[1,0] neg_lo:[1,0]
	v_add_u32_e32 v13, 0x15a80, v10
	v_pk_fma_f32 v[30:31], v[48:49], v[26:27], v[30:31] op_sel_hi:[0,1,1]
	ds_write_b64 v13, v[30:31]
	v_pk_mul_f32 v[30:31], v[178:179], v[26:27] op_sel:[1,1] op_sel_hi:[0,1] neg_lo:[0,1]
	v_pk_fma_f32 v[26:27], v[178:179], v[26:27], v[30:31] op_sel_hi:[1,0,1]
	s_nop 0
	v_pk_mul_f32 v[30:31], v[28:29], v[26:27] op_sel:[1,1] op_sel_hi:[1,0] neg_lo:[1,0]
	v_add_u32_e32 v13, 0x16b00, v10
	v_pk_fma_f32 v[28:29], v[28:29], v[26:27], v[30:31] op_sel_hi:[0,1,1]
	ds_write_b64 v13, v[28:29]
	v_pk_mul_f32 v[28:29], v[178:179], v[26:27] op_sel:[1,1] op_sel_hi:[0,1] neg_lo:[0,1]
	v_pk_fma_f32 v[26:27], v[178:179], v[26:27], v[28:29] op_sel_hi:[1,0,1]
	s_nop 0
	v_pk_mul_f32 v[28:29], v[52:53], v[26:27] op_sel:[1,1] op_sel_hi:[1,0] neg_lo:[1,0]
	v_add_u32_e32 v13, 0x17b80, v10
	v_pk_fma_f32 v[28:29], v[52:53], v[26:27], v[28:29] op_sel_hi:[0,1,1]
	ds_write_b64 v13, v[28:29]
	v_pk_mul_f32 v[28:29], v[178:179], v[26:27] op_sel:[1,1] op_sel_hi:[0,1] neg_lo:[0,1]
	v_pk_fma_f32 v[26:27], v[178:179], v[26:27], v[28:29] op_sel_hi:[1,0,1]
	s_nop 0
	v_pk_mul_f32 v[28:29], v[22:23], v[26:27] op_sel:[1,1] op_sel_hi:[1,0] neg_lo:[1,0]
	v_add_u32_e32 v13, 0x18c00, v10
	v_pk_fma_f32 v[22:23], v[22:23], v[26:27], v[28:29] op_sel_hi:[0,1,1]
	ds_write_b64 v13, v[22:23]
	v_pk_mul_f32 v[22:23], v[178:179], v[26:27] op_sel:[1,1] op_sel_hi:[0,1] neg_lo:[0,1]
	v_pk_fma_f32 v[22:23], v[178:179], v[26:27], v[22:23] op_sel_hi:[1,0,1]
	s_nop 0
	v_pk_mul_f32 v[26:27], v[38:39], v[22:23] op_sel:[1,1] op_sel_hi:[1,0] neg_lo:[1,0]
	v_add_u32_e32 v13, 0x19c80, v10
	v_pk_fma_f32 v[26:27], v[38:39], v[22:23], v[26:27] op_sel_hi:[0,1,1]
	ds_write_b64 v13, v[26:27]
	v_pk_mul_f32 v[26:27], v[178:179], v[22:23] op_sel:[1,1] op_sel_hi:[0,1] neg_lo:[0,1]
	v_pk_fma_f32 v[22:23], v[178:179], v[22:23], v[26:27] op_sel_hi:[1,0,1]
	s_nop 0
	v_pk_mul_f32 v[26:27], v[24:25], v[22:23] op_sel:[1,1] op_sel_hi:[1,0] neg_lo:[1,0]
	v_add_u32_e32 v13, 0x1ad00, v10
	v_pk_fma_f32 v[24:25], v[24:25], v[22:23], v[26:27] op_sel_hi:[0,1,1]
	ds_write_b64 v13, v[24:25]
	v_pk_mul_f32 v[24:25], v[178:179], v[22:23] op_sel:[1,1] op_sel_hi:[0,1] neg_lo:[0,1]
	v_pk_fma_f32 v[22:23], v[178:179], v[22:23], v[24:25] op_sel_hi:[1,0,1]
	s_nop 0
	v_pk_mul_f32 v[24:25], v[42:43], v[22:23] op_sel:[1,1] op_sel_hi:[1,0] neg_lo:[1,0]
	v_add_u32_e32 v13, 0x1bd80, v10
	v_pk_fma_f32 v[24:25], v[42:43], v[22:23], v[24:25] op_sel_hi:[0,1,1]
	ds_write_b64 v13, v[24:25]
	v_pk_mul_f32 v[24:25], v[178:179], v[22:23] op_sel:[1,1] op_sel_hi:[0,1] neg_lo:[0,1]
	v_pk_fma_f32 v[22:23], v[178:179], v[22:23], v[24:25] op_sel_hi:[1,0,1]
	s_nop 0
	v_pk_mul_f32 v[24:25], v[18:19], v[22:23] op_sel:[1,1] op_sel_hi:[1,0] neg_lo:[1,0]
	v_add_u32_e32 v13, 0x1ce00, v10
	v_pk_fma_f32 v[18:19], v[18:19], v[22:23], v[24:25] op_sel_hi:[0,1,1]
	ds_write_b64 v13, v[18:19]
	v_pk_mul_f32 v[18:19], v[178:179], v[22:23] op_sel:[1,1] op_sel_hi:[0,1] neg_lo:[0,1]
	v_pk_fma_f32 v[18:19], v[178:179], v[22:23], v[18:19] op_sel_hi:[1,0,1]
	s_nop 0
	v_pk_mul_f32 v[22:23], v[32:33], v[18:19] op_sel:[1,1] op_sel_hi:[1,0] neg_lo:[1,0]
	v_add_u32_e32 v13, 0x1de80, v10
	v_pk_fma_f32 v[22:23], v[32:33], v[18:19], v[22:23] op_sel_hi:[0,1,1]
	ds_write_b64 v13, v[22:23]
	v_pk_mul_f32 v[22:23], v[178:179], v[18:19] op_sel:[1,1] op_sel_hi:[0,1] neg_lo:[0,1]
	v_pk_fma_f32 v[18:19], v[178:179], v[18:19], v[22:23] op_sel_hi:[1,0,1]
	s_nop 0
	v_pk_mul_f32 v[22:23], v[20:21], v[18:19] op_sel:[1,1] op_sel_hi:[1,0] neg_lo:[1,0]
	v_add_u32_e32 v13, 0x1ef00, v10
	v_pk_fma_f32 v[20:21], v[20:21], v[18:19], v[22:23] op_sel_hi:[0,1,1]
	ds_write_b64 v13, v[20:21]
	v_pk_mul_f32 v[20:21], v[178:179], v[18:19] op_sel:[1,1] op_sel_hi:[0,1] neg_lo:[0,1]
	v_pk_fma_f32 v[16:17], v[178:179], v[18:19], v[20:21] op_sel_hi:[1,0,1]
	s_nop 0
	v_pk_mul_f32 v[18:19], v[36:37], v[16:17] op_sel:[1,1] op_sel_hi:[1,0] neg_lo:[1,0]
	v_add_u32_e32 v10, 0x1ff80, v10
	v_pk_fma_f32 v[16:17], v[36:37], v[16:17], v[18:19] op_sel_hi:[0,1,1]
	ds_write_b64 v10, v[16:17]
	v_mov_b32_e32 v10, v174
	v_mov_b32_e32 v13, v172
	s_waitcnt lgkmcnt(0)
	s_barrier
	v_mov_b32_e32 v16, v180
	v_add_u32_e32 v15, v13, v10
	v_lshl_add_u32 v75, v15, 3, 0
	v_xad_u32 v15, v13, 1, v10
	v_lshl_add_u32 v74, v15, 3, 0
	v_xad_u32 v15, v13, 2, v10
	v_lshl_add_u32 v73, v15, 3, 0
	v_xad_u32 v15, v13, 3, v10
	v_lshl_add_u32 v72, v15, 3, 0
	v_xad_u32 v15, v13, 4, v10
	v_lshl_add_u32 v71, v15, 3, 0
	v_xad_u32 v15, v13, 5, v10
	v_lshl_add_u32 v70, v15, 3, 0
	v_xad_u32 v15, v13, 6, v10
	v_lshl_add_u32 v69, v15, 3, 0
	v_xad_u32 v15, v13, 7, v10
	v_lshl_add_u32 v68, v15, 3, 0
	v_xad_u32 v15, v13, 8, v10
	v_lshl_add_u32 v15, v15, 3, 0
	v_add_u32_e32 v67, 0x800, v15
	v_xad_u32 v15, v13, 9, v10
	v_lshl_add_u32 v15, v15, 3, 0
	v_add_u32_e32 v66, 0x800, v15
	v_xad_u32 v15, v13, 10, v10
	v_lshl_add_u32 v15, v15, 3, 0
	v_add_u32_e32 v65, 0x800, v15
	v_xad_u32 v15, v13, 11, v10
	v_lshl_add_u32 v15, v15, 3, 0
	v_add_u32_e32 v64, 0x800, v15
	v_xad_u32 v15, v13, 12, v10
	v_mov_b32_e32 v17, v181
	v_lshl_add_u32 v15, v15, 3, 0
	ds_read2_b64 v[18:21], v75 offset1:16
	ds_read2_b64 v[40:43], v67 offset1:16
	v_add_u32_e32 v63, 0x800, v15
	v_xad_u32 v15, v13, 13, v10
	v_lshl_add_u32 v15, v15, 3, 0
	v_add_u32_e32 v62, 0x800, v15
	v_xad_u32 v15, v13, 14, v10
	v_xad_u32 v10, v13, 15, v10
	ds_read2_b64 v[22:25], v74 offset0:32 offset1:48
	ds_read2_b64 v[48:51], v66 offset0:32 offset1:48
	v_lshl_add_u32 v15, v15, 3, 0
	v_lshl_add_u32 v10, v10, 3, 0
	v_add_u32_e32 v15, 0x800, v15
	v_add_u32_e32 v13, 0x800, v10
	v_mov_b32_e32 v10, v1
	ds_read2_b64 v[26:29], v73 offset0:64 offset1:80
	ds_read2_b64 v[58:61], v72 offset0:96 offset1:112
	ds_read2_b64 v[76:79], v71 offset0:128 offset1:144
	ds_read2_b64 v[80:83], v70 offset0:160 offset1:176
	ds_read2_b64 v[84:87], v69 offset0:192 offset1:208
	ds_read2_b64 v[88:91], v68 offset0:224 offset1:240
	ds_read2_b64 v[54:57], v65 offset0:64 offset1:80
	ds_read2_b64 v[92:95], v64 offset0:96 offset1:112
	ds_read2_b64 v[96:99], v63 offset0:128 offset1:144
	ds_read2_b64 v[100:103], v62 offset0:160 offset1:176
	ds_read2_b64 v[104:107], v15 offset0:192 offset1:208
	ds_read2_b64 v[108:111], v13 offset0:224 offset1:240
	s_waitcnt lgkmcnt(14)
	v_pk_add_f32 v[112:113], v[18:19], v[40:41]
	v_pk_add_f32 v[40:41], v[18:19], v[40:41] neg_lo:[0,1] neg_hi:[0,1]
	v_pk_add_f32 v[18:19], v[20:21], v[42:43]
	v_pk_add_f32 v[20:21], v[20:21], v[42:43] neg_lo:[0,1] neg_hi:[0,1]
	v_mov_b32_e32 v30, v164
	v_mov_b32_e32 v32, v165
	v_mov_b32_e32 v34, v166
	v_mov_b32_e32 v10, v167
	v_mov_b32_e32 v38, v168
	v_mov_b32_e32 v36, v169
	v_mov_b32_e32 v46, v170
	v_mov_b32_e32 v31, v171
	v_pk_mul_f32 v[42:43], v[20:21], v[46:47] op_sel:[1,0] op_sel_hi:[0,0] neg_lo:[1,1] neg_hi:[0,1]
	s_nop 0
	v_pk_fma_f32 v[44:45], v[20:21], v[30:31], v[42:43] op_sel_hi:[1,0,1]
	s_waitcnt lgkmcnt(12)
	v_pk_add_f32 v[20:21], v[22:23], v[48:49]
	v_pk_add_f32 v[22:23], v[22:23], v[48:49] neg_lo:[0,1] neg_hi:[0,1]
	s_nop 0
	v_pk_mul_f32 v[42:43], v[22:23], v[36:37] op_sel:[1,0] op_sel_hi:[0,0] neg_lo:[1,1] neg_hi:[0,1]
	s_nop 0
	v_pk_fma_f32 v[48:49], v[22:23], v[32:33], v[42:43] op_sel_hi:[1,0,1]
	v_pk_add_f32 v[22:23], v[24:25], v[50:51]
	v_pk_add_f32 v[24:25], v[24:25], v[50:51] neg_lo:[0,1] neg_hi:[0,1]
	s_nop 0
	v_pk_mul_f32 v[42:43], v[24:25], v[38:39] op_sel:[1,0] op_sel_hi:[0,0] neg_lo:[1,1] neg_hi:[0,1]
	s_nop 0
	v_pk_fma_f32 v[52:53], v[24:25], v[34:35], v[42:43] op_sel_hi:[1,0,1]
	s_waitcnt lgkmcnt(5)
	v_pk_add_f32 v[24:25], v[26:27], v[54:55]
	v_pk_add_f32 v[26:27], v[26:27], v[54:55] neg_lo:[0,1] neg_hi:[0,1]
	s_nop 0
	v_pk_mul_f32 v[42:43], v[26:27], v[10:11] op_sel:[1,0] op_sel_hi:[0,0] neg_lo:[1,1] neg_hi:[0,1]
	s_nop 0
	v_pk_fma_f32 v[54:55], v[26:27], v[10:11], v[42:43] op_sel_hi:[1,0,1]
	v_pk_add_f32 v[26:27], v[28:29], v[56:57]
	v_pk_add_f32 v[28:29], v[28:29], v[56:57] neg_lo:[0,1] neg_hi:[0,1]
	s_nop 0
	v_pk_mul_f32 v[42:43], v[28:29], v[38:39] op_sel_hi:[1,0]
	s_nop 0
	v_pk_fma_f32 v[56:57], v[28:29], v[34:35], v[42:43] op_sel:[1,0,0] op_sel_hi:[0,0,1] neg_lo:[1,1,0] neg_hi:[0,1,0]
	s_waitcnt lgkmcnt(4)
	v_pk_add_f32 v[42:43], v[58:59], v[92:93] neg_lo:[0,1] neg_hi:[0,1]
	v_pk_add_f32 v[28:29], v[58:59], v[92:93]
	v_pk_mul_f32 v[50:51], v[42:43], v[36:37] op_sel_hi:[1,0]
	s_nop 0
	v_pk_fma_f32 v[58:59], v[42:43], v[32:33], v[50:51] op_sel:[1,0,0] op_sel_hi:[0,0,1] neg_lo:[1,1,0] neg_hi:[0,1,0]
	v_pk_add_f32 v[50:51], v[60:61], v[94:95] neg_lo:[0,1] neg_hi:[0,1]
	v_pk_add_f32 v[42:43], v[60:61], v[94:95]
	v_pk_mul_f32 v[60:61], v[50:51], v[46:47] op_sel_hi:[1,0]
	v_xor_b32_e32 v92, 0x80000000, v51
	v_mov_b32_e32 v93, v50
	s_waitcnt lgkmcnt(3)
	v_pk_add_f32 v[50:51], v[76:77], v[96:97]
	v_pk_add_f32 v[76:77], v[76:77], v[96:97] neg_lo:[0,1] neg_hi:[0,1]
	v_pk_fma_f32 v[60:61], v[92:93], v[30:31], v[60:61] op_sel_hi:[1,0,1] neg_lo:[0,1,0] neg_hi:[0,1,0]
	v_xor_b32_e32 v93, 0x80000000, v76
	v_mov_b32_e32 v92, v77
	v_pk_add_f32 v[76:77], v[78:79], v[98:99]
	v_pk_add_f32 v[78:79], v[78:79], v[98:99] neg_lo:[0,1] neg_hi:[0,1]
	s_nop 0
	v_pk_mul_f32 v[94:95], v[78:79], v[46:47] op_sel_hi:[1,0] neg_lo:[0,1] neg_hi:[0,1]
	s_nop 0
	v_pk_fma_f32 v[78:79], v[78:79], v[30:31], v[94:95] op_sel:[1,0,0] op_sel_hi:[0,0,1] neg_lo:[1,1,0] neg_hi:[0,1,0]
	s_waitcnt lgkmcnt(2)
	v_pk_add_f32 v[94:95], v[80:81], v[100:101]
	v_pk_add_f32 v[80:81], v[80:81], v[100:101] neg_lo:[0,1] neg_hi:[0,1]
	s_nop 0
	v_pk_mul_f32 v[96:97], v[80:81], v[36:37] op_sel_hi:[1,0] neg_lo:[0,1] neg_hi:[0,1]
	s_nop 0
	v_pk_fma_f32 v[80:81], v[80:81], v[32:33], v[96:97] op_sel:[1,0,0] op_sel_hi:[0,0,1] neg_lo:[1,1,0] neg_hi:[0,1,0]
	v_pk_add_f32 v[96:97], v[82:83], v[102:103]
	v_pk_add_f32 v[82:83], v[82:83], v[102:103] neg_lo:[0,1] neg_hi:[0,1]
	s_nop 0
	v_pk_mul_f32 v[98:99], v[82:83], v[38:39] op_sel_hi:[1,0] neg_lo:[0,1] neg_hi:[0,1]
	s_nop 0
	v_pk_fma_f32 v[82:83], v[82:83], v[34:35], v[98:99] op_sel:[1,0,0] op_sel_hi:[0,0,1] neg_lo:[1,1,0] neg_hi:[0,1,0]
	s_waitcnt lgkmcnt(1)
	v_pk_add_f32 v[98:99], v[84:85], v[104:105]
	v_pk_add_f32 v[84:85], v[84:85], v[104:105] neg_lo:[0,1] neg_hi:[0,1]
	s_nop 0
	v_pk_mul_f32 v[100:101], v[84:85], v[10:11] op_sel:[1,0] op_sel_hi:[0,0] neg_lo:[1,1] neg_hi:[0,1]
	s_nop 0
	v_pk_fma_f32 v[84:85], v[84:85], v[10:11], v[100:101] op_sel_hi:[1,0,1] neg_lo:[0,1,0] neg_hi:[0,1,0]
	v_pk_add_f32 v[100:101], v[86:87], v[106:107]
	v_pk_add_f32 v[86:87], v[86:87], v[106:107] neg_lo:[0,1] neg_hi:[0,1]
	s_nop 0
	v_pk_mul_f32 v[38:39], v[86:87], v[38:39] op_sel:[1,0] op_sel_hi:[0,0] neg_lo:[1,1] neg_hi:[0,1]
	s_nop 0
	v_pk_fma_f32 v[86:87], v[86:87], v[34:35], v[38:39] op_sel_hi:[1,0,1] neg_lo:[0,1,0] neg_hi:[0,1,0]
	s_waitcnt lgkmcnt(0)
	v_pk_add_f32 v[38:39], v[88:89], v[108:109] neg_lo:[0,1] neg_hi:[0,1]
	v_pk_add_f32 v[34:35], v[88:89], v[108:109]
	v_pk_mul_f32 v[88:89], v[38:39], v[36:37] op_sel:[1,0] op_sel_hi:[0,0] neg_lo:[1,1] neg_hi:[0,1]
	s_nop 0
	v_pk_fma_f32 v[88:89], v[38:39], v[32:33], v[88:89] op_sel_hi:[1,0,1] neg_lo:[0,1,0] neg_hi:[0,1,0]
	v_pk_add_f32 v[38:39], v[90:91], v[110:111]
	v_pk_add_f32 v[90:91], v[90:91], v[110:111] neg_lo:[0,1] neg_hi:[0,1]
	s_nop 0
	v_pk_mul_f32 v[46:47], v[90:91], v[46:47] op_sel:[1,0] op_sel_hi:[0,0] neg_lo:[1,1] neg_hi:[0,1]
	s_nop 0
	v_pk_fma_f32 v[90:91], v[90:91], v[30:31], v[46:47] op_sel_hi:[1,0,1] neg_lo:[0,1,0] neg_hi:[0,1,0]
	v_pk_add_f32 v[46:47], v[18:19], v[76:77]
	v_pk_add_f32 v[18:19], v[18:19], v[76:77] neg_lo:[0,1] neg_hi:[0,1]
	v_pk_add_f32 v[30:31], v[112:113], v[50:51]
	v_pk_mul_f32 v[76:77], v[18:19], v[36:37] op_sel:[1,0] op_sel_hi:[0,0] neg_lo:[1,1] neg_hi:[0,1]
	v_pk_add_f32 v[50:51], v[112:113], v[50:51] neg_lo:[0,1] neg_hi:[0,1]
	v_pk_fma_f32 v[76:77], v[18:19], v[32:33], v[76:77] op_sel_hi:[1,0,1]
	v_pk_add_f32 v[18:19], v[20:21], v[94:95]
	v_pk_add_f32 v[20:21], v[20:21], v[94:95] neg_lo:[0,1] neg_hi:[0,1]
	s_nop 0
	v_pk_mul_f32 v[94:95], v[20:21], v[10:11] op_sel:[1,0] op_sel_hi:[0,0] neg_lo:[1,1] neg_hi:[0,1]
	s_nop 0
	v_pk_fma_f32 v[20:21], v[20:21], v[10:11], v[94:95] op_sel_hi:[1,0,1]
	v_pk_add_f32 v[94:95], v[22:23], v[96:97]
	v_pk_add_f32 v[22:23], v[22:23], v[96:97] neg_lo:[0,1] neg_hi:[0,1]
	s_nop 0
	v_pk_mul_f32 v[96:97], v[22:23], v[36:37] op_sel_hi:[1,0]
	v_xor_b32_e32 v102, 0x80000000, v23
	v_mov_b32_e32 v103, v22
	v_pk_add_f32 v[22:23], v[24:25], v[98:99]
	v_pk_add_f32 v[24:25], v[24:25], v[98:99] neg_lo:[0,1] neg_hi:[0,1]
	v_pk_fma_f32 v[96:97], v[102:103], v[32:33], v[96:97] op_sel_hi:[1,0,1] neg_lo:[0,1,0] neg_hi:[0,1,0]
	v_xor_b32_e32 v99, 0x80000000, v24
	v_mov_b32_e32 v98, v25
	v_pk_add_f32 v[24:25], v[26:27], v[100:101]
	v_pk_add_f32 v[26:27], v[26:27], v[100:101] neg_lo:[0,1] neg_hi:[0,1]
	s_nop 0
	v_pk_mul_f32 v[100:101], v[26:27], v[36:37] op_sel_hi:[1,0] neg_lo:[0,1] neg_hi:[0,1]
	v_xor_b32_e32 v102, 0x80000000, v27
	v_mov_b32_e32 v103, v26
	v_pk_add_f32 v[26:27], v[28:29], v[34:35]
	v_pk_add_f32 v[28:29], v[28:29], v[34:35] neg_lo:[0,1] neg_hi:[0,1]
	v_pk_fma_f32 v[100:101], v[102:103], v[32:33], v[100:101] op_sel_hi:[1,0,1] neg_lo:[0,1,0] neg_hi:[0,1,0]
	v_pk_mul_f32 v[34:35], v[28:29], v[10:11] op_sel:[1,0] op_sel_hi:[0,0] neg_lo:[1,1] neg_hi:[0,1]
	v_pk_add_f32 v[102:103], v[30:31], v[22:23] neg_lo:[0,1] neg_hi:[0,1]
	v_pk_fma_f32 v[28:29], v[28:29], v[10:11], v[34:35] op_sel_hi:[1,0,1] neg_lo:[0,1,0] neg_hi:[0,1,0]
	v_pk_add_f32 v[34:35], v[42:43], v[38:39]
	v_pk_add_f32 v[38:39], v[42:43], v[38:39] neg_lo:[0,1] neg_hi:[0,1]
	s_nop 0
	v_pk_mul_f32 v[42:43], v[38:39], v[36:37] op_sel:[1,0] op_sel_hi:[0,0] neg_lo:[1,1] neg_hi:[0,1]
	s_nop 0
	v_pk_fma_f32 v[42:43], v[38:39], v[32:33], v[42:43] op_sel_hi:[1,0,1] neg_lo:[0,1,0] neg_hi:[0,1,0]
	v_pk_add_f32 v[38:39], v[30:31], v[22:23]
	v_pk_add_f32 v[22:23], v[46:47], v[24:25]
	v_pk_add_f32 v[24:25], v[46:47], v[24:25] neg_lo:[0,1] neg_hi:[0,1]
	s_nop 0
	v_pk_mul_f32 v[30:31], v[24:25], v[10:11] op_sel:[1,0] op_sel_hi:[0,0] neg_lo:[1,1] neg_hi:[0,1]
	s_nop 0
	v_pk_fma_f32 v[24:25], v[24:25], v[10:11], v[30:31] op_sel_hi:[1,0,1]
	v_pk_add_f32 v[30:31], v[18:19], v[26:27]
	v_pk_add_f32 v[18:19], v[18:19], v[26:27] neg_lo:[0,1] neg_hi:[0,1]
	s_nop 0
	v_xor_b32_e32 v27, 0x80000000, v18
	v_mov_b32_e32 v26, v19
	v_pk_add_f32 v[18:19], v[94:95], v[34:35]
	v_pk_add_f32 v[34:35], v[94:95], v[34:35] neg_lo:[0,1] neg_hi:[0,1]
	s_nop 0
	v_pk_mul_f32 v[46:47], v[34:35], v[10:11] op_sel:[1,0] op_sel_hi:[0,0] neg_lo:[1,1] neg_hi:[0,1]
	s_nop 0
	v_pk_fma_f32 v[34:35], v[34:35], v[10:11], v[46:47] op_sel_hi:[1,0,1] neg_lo:[0,1,0] neg_hi:[0,1,0]
	v_pk_add_f32 v[46:47], v[38:39], v[30:31]
	v_pk_add_f32 v[38:39], v[38:39], v[30:31] neg_lo:[0,1] neg_hi:[0,1]
	v_pk_add_f32 v[30:31], v[22:23], v[18:19]
	v_pk_add_f32 v[18:19], v[22:23], v[18:19] neg_lo:[0,1] neg_hi:[0,1]
	v_pk_add_f32 v[94:95], v[46:47], v[30:31]
	v_xor_b32_e32 v23, 0x80000000, v18
	v_mov_b32_e32 v22, v19
	v_pk_add_f32 v[18:19], v[102:103], v[26:27]
	v_pk_add_f32 v[102:103], v[102:103], v[26:27] neg_lo:[0,1] neg_hi:[0,1]
	v_pk_add_f32 v[26:27], v[24:25], v[34:35]
	v_pk_add_f32 v[24:25], v[24:25], v[34:35] neg_lo:[0,1] neg_hi:[0,1]
	v_pk_add_f32 v[30:31], v[46:47], v[30:31] neg_lo:[0,1] neg_hi:[0,1]
	v_xor_b32_e32 v35, 0x80000000, v24
	v_mov_b32_e32 v34, v25
	v_pk_add_f32 v[24:25], v[50:51], v[98:99]
	v_pk_add_f32 v[98:99], v[50:51], v[98:99] neg_lo:[0,1] neg_hi:[0,1]
	v_pk_add_f32 v[50:51], v[76:77], v[100:101] neg_lo:[0,1] neg_hi:[0,1]
	v_pk_add_f32 v[46:47], v[38:39], v[22:23]
	v_pk_add_f32 v[22:23], v[38:39], v[22:23] neg_lo:[0,1] neg_hi:[0,1]
	v_pk_add_f32 v[104:105], v[18:19], v[26:27]
	v_pk_add_f32 v[26:27], v[18:19], v[26:27] neg_lo:[0,1] neg_hi:[0,1]
	v_pk_add_f32 v[38:39], v[102:103], v[34:35]
	v_pk_add_f32 v[18:19], v[102:103], v[34:35] neg_lo:[0,1] neg_hi:[0,1]
	v_pk_add_f32 v[34:35], v[76:77], v[100:101]
	v_pk_mul_f32 v[76:77], v[10:11], v[50:51] op_sel:[0,1] op_sel_hi:[0,0] neg_lo:[1,1] neg_hi:[1,0]
	v_pk_fma_f32 v[76:77], v[10:11], v[50:51], v[76:77] op_sel_hi:[0,1,1]
	v_pk_add_f32 v[50:51], v[20:21], v[28:29]
	v_pk_add_f32 v[20:21], v[20:21], v[28:29] neg_lo:[0,1] neg_hi:[0,1]
	s_nop 0
	v_xor_b32_e32 v29, 0x80000000, v20
	v_mov_b32_e32 v28, v21
	v_pk_add_f32 v[20:21], v[96:97], v[42:43]
	v_pk_add_f32 v[42:43], v[96:97], v[42:43] neg_lo:[0,1] neg_hi:[0,1]
	s_nop 0
	v_pk_mul_f32 v[96:97], v[10:11], v[42:43] op_sel:[0,1] op_sel_hi:[0,0] neg_lo:[1,1] neg_hi:[1,0]
	v_pk_fma_f32 v[42:43], v[10:11], v[42:43], v[96:97] op_sel_hi:[0,1,1] neg_lo:[1,0,0] neg_hi:[1,0,0]
	v_pk_add_f32 v[96:97], v[24:25], v[50:51]
	v_pk_add_f32 v[24:25], v[24:25], v[50:51] neg_lo:[0,1] neg_hi:[0,1]
	v_pk_add_f32 v[50:51], v[34:35], v[20:21]
	v_pk_add_f32 v[20:21], v[34:35], v[20:21] neg_lo:[0,1] neg_hi:[0,1]
	v_pk_add_f32 v[102:103], v[96:97], v[50:51]
	v_xor_b32_e32 v101, 0x80000000, v20
	v_mov_b32_e32 v100, v21
	v_pk_add_f32 v[34:35], v[96:97], v[50:51] neg_lo:[0,1] neg_hi:[0,1]
	v_pk_add_f32 v[20:21], v[98:99], v[28:29]
	v_pk_add_f32 v[96:97], v[98:99], v[28:29] neg_lo:[0,1] neg_hi:[0,1]
	v_pk_add_f32 v[28:29], v[76:77], v[42:43]
	v_pk_add_f32 v[42:43], v[76:77], v[42:43] neg_lo:[0,1] neg_hi:[0,1]
	v_pk_add_f32 v[98:99], v[20:21], v[28:29]
	v_xor_b32_e32 v77, 0x80000000, v42
	v_mov_b32_e32 v76, v43
	v_pk_add_f32 v[28:29], v[20:21], v[28:29] neg_lo:[0,1] neg_hi:[0,1]
	v_pk_add_f32 v[42:43], v[96:97], v[76:77]
	v_pk_add_f32 v[20:21], v[96:97], v[76:77] neg_lo:[0,1] neg_hi:[0,1]
	v_pk_add_f32 v[76:77], v[40:41], v[92:93]
	v_pk_add_f32 v[92:93], v[40:41], v[92:93] neg_lo:[0,1] neg_hi:[0,1]
	v_pk_add_f32 v[40:41], v[44:45], v[78:79]
	v_pk_add_f32 v[44:45], v[44:45], v[78:79] neg_lo:[0,1] neg_hi:[0,1]
	v_pk_add_f32 v[50:51], v[24:25], v[100:101]
	v_pk_mul_f32 v[78:79], v[36:37], v[44:45] op_sel:[0,1] op_sel_hi:[0,0] neg_lo:[1,1] neg_hi:[1,0]
	v_pk_fma_f32 v[44:45], v[32:33], v[44:45], v[78:79] op_sel_hi:[0,1,1]
	v_pk_add_f32 v[78:79], v[48:49], v[80:81]
	v_pk_add_f32 v[48:49], v[48:49], v[80:81] neg_lo:[0,1] neg_hi:[0,1]
	v_pk_add_f32 v[24:25], v[24:25], v[100:101] neg_lo:[0,1] neg_hi:[0,1]
	v_pk_mul_f32 v[80:81], v[10:11], v[48:49] op_sel:[0,1] op_sel_hi:[0,0] neg_lo:[1,1] neg_hi:[1,0]
	v_pk_fma_f32 v[80:81], v[10:11], v[48:49], v[80:81] op_sel_hi:[0,1,1]
	v_pk_add_f32 v[48:49], v[52:53], v[82:83]
	v_pk_add_f32 v[52:53], v[52:53], v[82:83] neg_lo:[0,1] neg_hi:[0,1]
	s_nop 0
	v_pk_mul_f32 v[82:83], v[32:33], v[52:53] op_sel:[0,1] op_sel_hi:[0,0] neg_lo:[1,1] neg_hi:[1,0]
	v_pk_fma_f32 v[52:53], v[36:37], v[52:53], v[82:83] op_sel_hi:[0,1,1]
	v_pk_add_f32 v[82:83], v[54:55], v[84:85]
	v_pk_add_f32 v[54:55], v[54:55], v[84:85] neg_lo:[0,1] neg_hi:[0,1]
	s_nop 0
	v_xor_b32_e32 v85, 0x80000000, v54
	v_mov_b32_e32 v84, v55
	v_pk_add_f32 v[54:55], v[56:57], v[86:87]
	v_pk_add_f32 v[56:57], v[56:57], v[86:87] neg_lo:[0,1] neg_hi:[0,1]
	s_nop 0
	v_pk_mul_f32 v[86:87], v[32:33], v[56:57] op_sel:[0,1] op_sel_hi:[0,0] neg_lo:[1,1] neg_hi:[1,0]
	v_pk_fma_f32 v[56:57], v[36:37], v[56:57], v[86:87] op_sel_hi:[0,1,1] neg_lo:[1,0,0] neg_hi:[1,0,0]
	v_pk_add_f32 v[86:87], v[58:59], v[88:89]
	v_pk_add_f32 v[58:59], v[58:59], v[88:89] neg_lo:[0,1] neg_hi:[0,1]
	s_nop 0
	v_pk_mul_f32 v[88:89], v[10:11], v[58:59] op_sel:[0,1] op_sel_hi:[0,0] neg_lo:[1,1] neg_hi:[1,0]
	v_pk_fma_f32 v[58:59], v[10:11], v[58:59], v[88:89] op_sel_hi:[0,1,1] neg_lo:[1,0,0] neg_hi:[1,0,0]
	v_pk_add_f32 v[88:89], v[60:61], v[90:91]
	v_pk_add_f32 v[60:61], v[60:61], v[90:91] neg_lo:[0,1] neg_hi:[0,1]
	s_nop 0
	v_pk_mul_f32 v[36:37], v[36:37], v[60:61] op_sel:[0,1] op_sel_hi:[0,0] neg_lo:[1,1] neg_hi:[1,0]
	v_pk_fma_f32 v[36:37], v[32:33], v[60:61], v[36:37] op_sel_hi:[0,1,1] neg_lo:[1,0,0] neg_hi:[1,0,0]
	v_pk_add_f32 v[32:33], v[76:77], v[82:83]
	v_pk_add_f32 v[60:61], v[76:77], v[82:83] neg_lo:[0,1] neg_hi:[0,1]
	v_pk_add_f32 v[76:77], v[54:55], v[40:41]
	v_pk_add_f32 v[40:41], v[40:41], v[54:55] neg_lo:[0,1] neg_hi:[0,1]
	s_nop 0
	v_pk_mul_f32 v[54:55], v[10:11], v[40:41] op_sel:[0,1] op_sel_hi:[0,0] neg_lo:[1,1] neg_hi:[1,0]
	v_pk_fma_f32 v[54:55], v[10:11], v[40:41], v[54:55] op_sel_hi:[0,1,1]
	v_pk_add_f32 v[40:41], v[78:79], v[86:87]
	v_pk_add_f32 v[78:79], v[78:79], v[86:87] neg_lo:[0,1] neg_hi:[0,1]
	s_nop 0
	v_xor_b32_e32 v83, 0x80000000, v78
	v_mov_b32_e32 v82, v79
	v_pk_add_f32 v[78:79], v[48:49], v[88:89]
	v_pk_add_f32 v[48:49], v[48:49], v[88:89] neg_lo:[0,1] neg_hi:[0,1]
	v_pk_add_f32 v[88:89], v[76:77], v[78:79]
	v_pk_mul_f32 v[86:87], v[10:11], v[48:49] op_sel:[0,1] op_sel_hi:[0,0] neg_lo:[1,1] neg_hi:[1,0]
	v_pk_fma_f32 v[48:49], v[10:11], v[48:49], v[86:87] op_sel_hi:[0,1,1] neg_lo:[1,0,0] neg_hi:[1,0,0]
	v_pk_add_f32 v[86:87], v[32:33], v[40:41]
	v_pk_add_f32 v[32:33], v[32:33], v[40:41] neg_lo:[0,1] neg_hi:[0,1]
	v_pk_add_f32 v[40:41], v[76:77], v[78:79] neg_lo:[0,1] neg_hi:[0,1]
	v_pk_add_f32 v[78:79], v[86:87], v[88:89] neg_lo:[0,1] neg_hi:[0,1]
	v_pk_add_f32 v[90:91], v[32:33], v[40:41] op_sel:[0,1] op_sel_hi:[1,0] neg_hi:[0,1]
	v_pk_add_f32 v[40:41], v[32:33], v[40:41] op_sel:[0,1] op_sel_hi:[1,0] neg_lo:[0,1]
	v_pk_add_f32 v[76:77], v[54:55], v[48:49]
	v_pk_add_f32 v[48:49], v[54:55], v[48:49] neg_lo:[0,1] neg_hi:[0,1]
	v_pk_add_f32 v[32:33], v[60:61], v[82:83]
	v_pk_add_f32 v[60:61], v[60:61], v[82:83] neg_lo:[0,1] neg_hi:[0,1]
	v_xor_b32_e32 v55, 0x80000000, v48
	v_mov_b32_e32 v54, v49
	v_pk_add_f32 v[82:83], v[32:33], v[76:77]
	v_pk_add_f32 v[48:49], v[32:33], v[76:77] neg_lo:[0,1] neg_hi:[0,1]
	v_pk_add_f32 v[76:77], v[60:61], v[54:55]
	v_pk_add_f32 v[32:33], v[60:61], v[54:55] neg_lo:[0,1] neg_hi:[0,1]
	v_pk_add_f32 v[54:55], v[92:93], v[84:85]
	v_pk_add_f32 v[60:61], v[92:93], v[84:85] neg_lo:[0,1] neg_hi:[0,1]
	v_pk_add_f32 v[84:85], v[56:57], v[44:45]
	v_pk_add_f32 v[44:45], v[44:45], v[56:57] neg_lo:[0,1] neg_hi:[0,1]
	v_pk_add_f32 v[86:87], v[86:87], v[88:89]
	v_pk_mul_f32 v[56:57], v[10:11], v[44:45] op_sel:[0,1] op_sel_hi:[0,0] neg_lo:[1,1] neg_hi:[1,0]
	v_pk_fma_f32 v[56:57], v[10:11], v[44:45], v[56:57] op_sel_hi:[0,1,1]
	v_pk_add_f32 v[44:45], v[80:81], v[58:59]
	v_pk_add_f32 v[58:59], v[80:81], v[58:59] neg_lo:[0,1] neg_hi:[0,1]
	s_nop 0
	v_xor_b32_e32 v81, 0x80000000, v58
	v_mov_b32_e32 v80, v59
	v_pk_add_f32 v[58:59], v[52:53], v[36:37]
	v_pk_add_f32 v[36:37], v[52:53], v[36:37] neg_lo:[0,1] neg_hi:[0,1]
	s_nop 0
	v_pk_mul_f32 v[52:53], v[10:11], v[36:37] op_sel:[0,1] op_sel_hi:[0,0] neg_lo:[1,1] neg_hi:[1,0]
	v_pk_fma_f32 v[36:37], v[10:11], v[36:37], v[52:53] op_sel_hi:[0,1,1] neg_lo:[1,0,0] neg_hi:[1,0,0]
	v_pk_add_f32 v[52:53], v[54:55], v[44:45]
	v_pk_add_f32 v[44:45], v[54:55], v[44:45] neg_lo:[0,1] neg_hi:[0,1]
	v_pk_add_f32 v[54:55], v[84:85], v[58:59]
	v_pk_add_f32 v[58:59], v[84:85], v[58:59] neg_lo:[0,1] neg_hi:[0,1]
	s_nop 0
	v_xor_b32_e32 v85, 0x80000000, v58
	v_mov_b32_e32 v84, v59
	v_pk_add_f32 v[58:59], v[52:53], v[54:55]
	v_pk_add_f32 v[52:53], v[52:53], v[54:55] neg_lo:[0,1] neg_hi:[0,1]
	v_pk_add_f32 v[54:55], v[44:45], v[84:85]
	v_pk_add_f32 v[44:45], v[44:45], v[84:85] neg_lo:[0,1] neg_hi:[0,1]
	v_pk_add_f32 v[84:85], v[60:61], v[80:81]
	v_pk_add_f32 v[60:61], v[60:61], v[80:81] neg_lo:[0,1] neg_hi:[0,1]
	v_pk_add_f32 v[80:81], v[56:57], v[36:37]
	v_pk_add_f32 v[36:37], v[56:57], v[36:37] neg_lo:[0,1] neg_hi:[0,1]
	v_pk_add_f32 v[92:93], v[84:85], v[80:81]
	v_pk_add_f32 v[80:81], v[84:85], v[80:81] neg_lo:[0,1] neg_hi:[0,1]
	v_pk_add_f32 v[84:85], v[60:61], v[36:37] op_sel:[0,1] op_sel_hi:[1,0] neg_hi:[0,1]
	v_pk_add_f32 v[36:37], v[60:61], v[36:37] op_sel:[0,1] op_sel_hi:[1,0] neg_lo:[0,1]
	v_pk_fma_f32 v[60:61], v[16:17], s[90:91], v[16:17] op_sel:[1,0,0] op_sel_hi:[0,1,1]
	v_pk_mul_f32 v[56:57], v[94:95], s[14:15] op_sel:[1,0] neg_lo:[1,0]
	v_pk_mul_f32 v[88:89], v[60:61], v[86:87] op_sel:[1,1] op_sel_hi:[0,1] neg_lo:[0,1]
	v_pk_fma_f32 v[56:57], v[94:95], s[94:95], v[56:57] op_sel_hi:[0,1,1]
	v_pk_fma_f32 v[86:87], v[60:61], v[86:87], v[88:89] op_sel_hi:[1,0,1]
	ds_write2_b64 v75, v[56:57], v[86:87] offset1:16
	v_pk_mul_f32 v[56:57], v[16:17], v[60:61] op_sel:[1,1] op_sel_hi:[0,1] neg_lo:[0,1]
	v_pk_fma_f32 v[56:57], v[16:17], v[60:61], v[56:57] op_sel_hi:[1,0,1]
	s_nop 0
	v_pk_mul_f32 v[60:61], v[56:57], v[102:103] op_sel:[1,1] op_sel_hi:[0,1] neg_lo:[0,1]
	v_pk_mul_f32 v[86:87], v[16:17], v[56:57] op_sel:[1,1] op_sel_hi:[0,1] neg_lo:[0,1]
	v_pk_fma_f32 v[60:61], v[56:57], v[102:103], v[60:61] op_sel_hi:[1,0,1]
	v_pk_fma_f32 v[56:57], v[16:17], v[56:57], v[86:87] op_sel_hi:[1,0,1]
	s_nop 0
	v_pk_mul_f32 v[86:87], v[56:57], v[58:59] op_sel:[1,1] op_sel_hi:[0,1] neg_lo:[0,1]
	v_pk_fma_f32 v[58:59], v[56:57], v[58:59], v[86:87] op_sel_hi:[1,0,1]
	ds_write2_b64 v74, v[60:61], v[58:59] offset0:32 offset1:48
	v_pk_mul_f32 v[58:59], v[16:17], v[56:57] op_sel:[1,1] op_sel_hi:[0,1] neg_lo:[0,1]
	v_pk_fma_f32 v[56:57], v[16:17], v[56:57], v[58:59] op_sel_hi:[1,0,1]
	s_nop 0
	v_pk_mul_f32 v[58:59], v[56:57], v[104:105] op_sel:[1,1] op_sel_hi:[0,1] neg_lo:[0,1]
	v_pk_mul_f32 v[60:61], v[16:17], v[56:57] op_sel:[1,1] op_sel_hi:[0,1] neg_lo:[0,1]
	v_pk_fma_f32 v[58:59], v[56:57], v[104:105], v[58:59] op_sel_hi:[1,0,1]
	v_pk_fma_f32 v[56:57], v[16:17], v[56:57], v[60:61] op_sel_hi:[1,0,1]
	s_nop 0
	v_pk_mul_f32 v[60:61], v[56:57], v[82:83] op_sel:[1,1] op_sel_hi:[0,1] neg_lo:[0,1]
	v_pk_fma_f32 v[60:61], v[56:57], v[82:83], v[60:61] op_sel_hi:[1,0,1]
	ds_write2_b64 v73, v[58:59], v[60:61] offset0:64 offset1:80
	v_pk_mul_f32 v[58:59], v[16:17], v[56:57] op_sel:[1,1] op_sel_hi:[0,1] neg_lo:[0,1]
	v_pk_fma_f32 v[56:57], v[16:17], v[56:57], v[58:59] op_sel_hi:[1,0,1]
	s_nop 0
	v_pk_mul_f32 v[58:59], v[56:57], v[98:99] op_sel:[1,1] op_sel_hi:[0,1] neg_lo:[0,1]
	v_pk_mul_f32 v[60:61], v[16:17], v[56:57] op_sel:[1,1] op_sel_hi:[0,1] neg_lo:[0,1]
	v_pk_fma_f32 v[58:59], v[56:57], v[98:99], v[58:59] op_sel_hi:[1,0,1]
	v_pk_fma_f32 v[56:57], v[16:17], v[56:57], v[60:61] op_sel_hi:[1,0,1]
	s_nop 0
	v_pk_mul_f32 v[60:61], v[56:57], v[92:93] op_sel:[1,1] op_sel_hi:[0,1] neg_lo:[0,1]
	v_pk_fma_f32 v[60:61], v[56:57], v[92:93], v[60:61] op_sel_hi:[1,0,1]
	ds_write2_b64 v72, v[58:59], v[60:61] offset0:96 offset1:112
	v_pk_mul_f32 v[58:59], v[16:17], v[56:57] op_sel:[1,1] op_sel_hi:[0,1] neg_lo:[0,1]
	v_pk_fma_f32 v[56:57], v[16:17], v[56:57], v[58:59] op_sel_hi:[1,0,1]
	s_nop 0
	v_pk_mul_f32 v[58:59], v[56:57], v[46:47] op_sel:[1,1] op_sel_hi:[0,1] neg_lo:[0,1]
	v_pk_fma_f32 v[46:47], v[56:57], v[46:47], v[58:59] op_sel_hi:[1,0,1]
	v_pk_mul_f32 v[58:59], v[16:17], v[56:57] op_sel:[1,1] op_sel_hi:[0,1] neg_lo:[0,1]
	v_pk_fma_f32 v[56:57], v[16:17], v[56:57], v[58:59] op_sel_hi:[1,0,1]
	s_nop 0
	v_pk_mul_f32 v[58:59], v[56:57], v[90:91] op_sel:[1,1] op_sel_hi:[0,1] neg_lo:[0,1]
	v_pk_fma_f32 v[58:59], v[56:57], v[90:91], v[58:59] op_sel_hi:[1,0,1]
	ds_write2_b64 v71, v[46:47], v[58:59] offset0:128 offset1:144
	v_pk_mul_f32 v[46:47], v[16:17], v[56:57] op_sel:[1,1] op_sel_hi:[0,1] neg_lo:[0,1]
	v_pk_fma_f32 v[46:47], v[16:17], v[56:57], v[46:47] op_sel_hi:[1,0,1]
	s_nop 0
	v_pk_mul_f32 v[56:57], v[46:47], v[50:51] op_sel:[1,1] op_sel_hi:[0,1] neg_lo:[0,1]
	v_pk_fma_f32 v[50:51], v[46:47], v[50:51], v[56:57] op_sel_hi:[1,0,1]
	v_pk_mul_f32 v[56:57], v[16:17], v[46:47] op_sel:[1,1] op_sel_hi:[0,1] neg_lo:[0,1]
	v_pk_fma_f32 v[46:47], v[16:17], v[46:47], v[56:57] op_sel_hi:[1,0,1]
	s_nop 0
	v_pk_mul_f32 v[56:57], v[46:47], v[54:55] op_sel:[1,1] op_sel_hi:[0,1] neg_lo:[0,1]
	v_pk_fma_f32 v[54:55], v[46:47], v[54:55], v[56:57] op_sel_hi:[1,0,1]
	ds_write2_b64 v70, v[50:51], v[54:55] offset0:160 offset1:176
	v_pk_mul_f32 v[50:51], v[16:17], v[46:47] op_sel:[1,1] op_sel_hi:[0,1] neg_lo:[0,1]
	v_pk_fma_f32 v[46:47], v[16:17], v[46:47], v[50:51] op_sel_hi:[1,0,1]
	s_nop 0
	v_pk_mul_f32 v[50:51], v[38:39], v[46:47] op_sel:[1,1] op_sel_hi:[1,0] neg_lo:[1,0]
	s_nop 0
	v_pk_fma_f32 v[38:39], v[38:39], v[46:47], v[50:51] op_sel_hi:[0,1,1]
	v_pk_mul_f32 v[50:51], v[16:17], v[46:47] op_sel:[1,1] op_sel_hi:[0,1] neg_lo:[0,1]
	v_pk_fma_f32 v[46:47], v[16:17], v[46:47], v[50:51] op_sel_hi:[1,0,1]
	s_nop 0
	v_pk_mul_f32 v[50:51], v[46:47], v[76:77] op_sel:[1,1] op_sel_hi:[0,1] neg_lo:[0,1]
	v_pk_fma_f32 v[50:51], v[46:47], v[76:77], v[50:51] op_sel_hi:[1,0,1]
	ds_write2_b64 v69, v[38:39], v[50:51] offset0:192 offset1:208
	v_pk_mul_f32 v[38:39], v[16:17], v[46:47] op_sel:[1,1] op_sel_hi:[0,1] neg_lo:[0,1]
	v_pk_fma_f32 v[38:39], v[16:17], v[46:47], v[38:39] op_sel_hi:[1,0,1]
	s_nop 0
	v_pk_mul_f32 v[46:47], v[42:43], v[38:39] op_sel:[1,1] op_sel_hi:[1,0] neg_lo:[1,0]
	s_nop 0
	v_pk_fma_f32 v[42:43], v[42:43], v[38:39], v[46:47] op_sel_hi:[0,1,1]
	v_pk_mul_f32 v[46:47], v[16:17], v[38:39] op_sel:[1,1] op_sel_hi:[0,1] neg_lo:[0,1]
	v_pk_fma_f32 v[38:39], v[16:17], v[38:39], v[46:47] op_sel_hi:[1,0,1]
	s_nop 0
	v_pk_mul_f32 v[46:47], v[38:39], v[84:85] op_sel:[1,1] op_sel_hi:[0,1] neg_lo:[0,1]
	v_pk_fma_f32 v[46:47], v[38:39], v[84:85], v[46:47] op_sel_hi:[1,0,1]
	ds_write2_b64 v68, v[42:43], v[46:47] offset0:224 offset1:240
	v_pk_mul_f32 v[42:43], v[16:17], v[38:39] op_sel:[1,1] op_sel_hi:[0,1] neg_lo:[0,1]
	v_pk_fma_f32 v[38:39], v[16:17], v[38:39], v[42:43] op_sel_hi:[1,0,1]
	s_nop 0
	v_pk_mul_f32 v[42:43], v[30:31], v[38:39] op_sel:[1,1] op_sel_hi:[1,0] neg_lo:[1,0]
	s_nop 0
	v_pk_fma_f32 v[30:31], v[30:31], v[38:39], v[42:43] op_sel_hi:[0,1,1]
	v_pk_mul_f32 v[42:43], v[16:17], v[38:39] op_sel:[1,1] op_sel_hi:[0,1] neg_lo:[0,1]
	v_pk_fma_f32 v[38:39], v[16:17], v[38:39], v[42:43] op_sel_hi:[1,0,1]
	s_nop 0
	v_pk_mul_f32 v[42:43], v[78:79], v[38:39] op_sel:[1,1] op_sel_hi:[1,0] neg_lo:[1,0]
	s_nop 0
	v_pk_fma_f32 v[42:43], v[78:79], v[38:39], v[42:43] op_sel_hi:[0,1,1]
	ds_write2_b64 v67, v[30:31], v[42:43] offset1:16
	v_pk_mul_f32 v[30:31], v[16:17], v[38:39] op_sel:[1,1] op_sel_hi:[0,1] neg_lo:[0,1]
	v_pk_fma_f32 v[30:31], v[16:17], v[38:39], v[30:31] op_sel_hi:[1,0,1]
	s_nop 0
	v_pk_mul_f32 v[38:39], v[34:35], v[30:31] op_sel:[1,1] op_sel_hi:[1,0] neg_lo:[1,0]
	s_nop 0
	v_pk_fma_f32 v[34:35], v[34:35], v[30:31], v[38:39] op_sel_hi:[0,1,1]
	v_pk_mul_f32 v[38:39], v[16:17], v[30:31] op_sel:[1,1] op_sel_hi:[0,1] neg_lo:[0,1]
	v_pk_fma_f32 v[30:31], v[16:17], v[30:31], v[38:39] op_sel_hi:[1,0,1]
	s_nop 0
	v_pk_mul_f32 v[38:39], v[52:53], v[30:31] op_sel:[1,1] op_sel_hi:[1,0] neg_lo:[1,0]
	s_nop 0
	v_pk_fma_f32 v[38:39], v[52:53], v[30:31], v[38:39] op_sel_hi:[0,1,1]
	ds_write2_b64 v66, v[34:35], v[38:39] offset0:32 offset1:48
	v_pk_mul_f32 v[34:35], v[16:17], v[30:31] op_sel:[1,1] op_sel_hi:[0,1] neg_lo:[0,1]
	v_pk_fma_f32 v[30:31], v[16:17], v[30:31], v[34:35] op_sel_hi:[1,0,1]
	s_nop 0
	v_pk_mul_f32 v[34:35], v[26:27], v[30:31] op_sel:[1,1] op_sel_hi:[1,0] neg_lo:[1,0]
	s_nop 0
	v_pk_fma_f32 v[26:27], v[26:27], v[30:31], v[34:35] op_sel_hi:[0,1,1]
	v_pk_mul_f32 v[34:35], v[16:17], v[30:31] op_sel:[1,1] op_sel_hi:[0,1] neg_lo:[0,1]
	v_pk_fma_f32 v[30:31], v[16:17], v[30:31], v[34:35] op_sel_hi:[1,0,1]
	s_nop 0
	v_pk_mul_f32 v[34:35], v[48:49], v[30:31] op_sel:[1,1] op_sel_hi:[1,0] neg_lo:[1,0]
	s_nop 0
	v_pk_fma_f32 v[34:35], v[48:49], v[30:31], v[34:35] op_sel_hi:[0,1,1]
	ds_write2_b64 v65, v[26:27], v[34:35] offset0:64 offset1:80
	v_pk_mul_f32 v[26:27], v[16:17], v[30:31] op_sel:[1,1] op_sel_hi:[0,1] neg_lo:[0,1]
	v_pk_fma_f32 v[26:27], v[16:17], v[30:31], v[26:27] op_sel_hi:[1,0,1]
	s_nop 0
	v_pk_mul_f32 v[30:31], v[28:29], v[26:27] op_sel:[1,1] op_sel_hi:[1,0] neg_lo:[1,0]
	s_nop 0
	v_pk_fma_f32 v[28:29], v[28:29], v[26:27], v[30:31] op_sel_hi:[0,1,1]
	v_pk_mul_f32 v[30:31], v[16:17], v[26:27] op_sel:[1,1] op_sel_hi:[0,1] neg_lo:[0,1]
	v_pk_fma_f32 v[26:27], v[16:17], v[26:27], v[30:31] op_sel_hi:[1,0,1]
	s_nop 0
	v_pk_mul_f32 v[30:31], v[80:81], v[26:27] op_sel:[1,1] op_sel_hi:[1,0] neg_lo:[1,0]
	s_nop 0
	v_pk_fma_f32 v[30:31], v[80:81], v[26:27], v[30:31] op_sel_hi:[0,1,1]
	ds_write2_b64 v64, v[28:29], v[30:31] offset0:96 offset1:112
	v_pk_mul_f32 v[28:29], v[16:17], v[26:27] op_sel:[1,1] op_sel_hi:[0,1] neg_lo:[0,1]
	v_pk_fma_f32 v[26:27], v[16:17], v[26:27], v[28:29] op_sel_hi:[1,0,1]
	s_nop 0
	v_pk_mul_f32 v[28:29], v[22:23], v[26:27] op_sel:[1,1] op_sel_hi:[1,0] neg_lo:[1,0]
	s_nop 0
	v_pk_fma_f32 v[22:23], v[22:23], v[26:27], v[28:29] op_sel_hi:[0,1,1]
	v_pk_mul_f32 v[28:29], v[16:17], v[26:27] op_sel:[1,1] op_sel_hi:[0,1] neg_lo:[0,1]
	v_pk_fma_f32 v[26:27], v[16:17], v[26:27], v[28:29] op_sel_hi:[1,0,1]
	s_nop 0
	v_pk_mul_f32 v[28:29], v[40:41], v[26:27] op_sel:[1,1] op_sel_hi:[1,0] neg_lo:[1,0]
	s_nop 0
	v_pk_fma_f32 v[28:29], v[40:41], v[26:27], v[28:29] op_sel_hi:[0,1,1]
	ds_write2_b64 v63, v[22:23], v[28:29] offset0:128 offset1:144
	v_pk_mul_f32 v[22:23], v[16:17], v[26:27] op_sel:[1,1] op_sel_hi:[0,1] neg_lo:[0,1]
	v_pk_fma_f32 v[22:23], v[16:17], v[26:27], v[22:23] op_sel_hi:[1,0,1]
	s_nop 0
	v_pk_mul_f32 v[26:27], v[24:25], v[22:23] op_sel:[1,1] op_sel_hi:[1,0] neg_lo:[1,0]
	s_nop 0
	v_pk_fma_f32 v[24:25], v[24:25], v[22:23], v[26:27] op_sel_hi:[0,1,1]
	v_pk_mul_f32 v[26:27], v[16:17], v[22:23] op_sel:[1,1] op_sel_hi:[0,1] neg_lo:[0,1]
	v_pk_fma_f32 v[22:23], v[16:17], v[22:23], v[26:27] op_sel_hi:[1,0,1]
	s_nop 0
	v_pk_mul_f32 v[26:27], v[44:45], v[22:23] op_sel:[1,1] op_sel_hi:[1,0] neg_lo:[1,0]
	s_nop 0
	v_pk_fma_f32 v[26:27], v[44:45], v[22:23], v[26:27] op_sel_hi:[0,1,1]
	ds_write2_b64 v62, v[24:25], v[26:27] offset0:160 offset1:176
	v_pk_mul_f32 v[24:25], v[16:17], v[22:23] op_sel:[1,1] op_sel_hi:[0,1] neg_lo:[0,1]
	v_pk_fma_f32 v[22:23], v[16:17], v[22:23], v[24:25] op_sel_hi:[1,0,1]
	s_nop 0
	v_pk_mul_f32 v[24:25], v[18:19], v[22:23] op_sel:[1,1] op_sel_hi:[1,0] neg_lo:[1,0]
	s_nop 0
	v_pk_fma_f32 v[18:19], v[18:19], v[22:23], v[24:25] op_sel_hi:[0,1,1]
	v_pk_mul_f32 v[24:25], v[16:17], v[22:23] op_sel:[1,1] op_sel_hi:[0,1] neg_lo:[0,1]
	v_pk_fma_f32 v[22:23], v[16:17], v[22:23], v[24:25] op_sel_hi:[1,0,1]
	s_nop 0
	v_pk_mul_f32 v[24:25], v[32:33], v[22:23] op_sel:[1,1] op_sel_hi:[1,0] neg_lo:[1,0]
	s_nop 0
	v_pk_fma_f32 v[24:25], v[32:33], v[22:23], v[24:25] op_sel_hi:[0,1,1]
	ds_write2_b64 v15, v[18:19], v[24:25] offset0:192 offset1:208
	v_pk_mul_f32 v[18:19], v[16:17], v[22:23] op_sel:[1,1] op_sel_hi:[0,1] neg_lo:[0,1]
	v_pk_fma_f32 v[18:19], v[16:17], v[22:23], v[18:19] op_sel_hi:[1,0,1]
	s_nop 0
	v_pk_mul_f32 v[22:23], v[20:21], v[18:19] op_sel:[1,1] op_sel_hi:[1,0] neg_lo:[1,0]
	s_nop 0
	v_pk_fma_f32 v[20:21], v[20:21], v[18:19], v[22:23] op_sel_hi:[0,1,1]
	v_pk_mul_f32 v[22:23], v[16:17], v[18:19] op_sel:[1,1] op_sel_hi:[0,1] neg_lo:[0,1]
	v_pk_fma_f32 v[16:17], v[16:17], v[18:19], v[22:23] op_sel_hi:[1,0,1]
	s_nop 0
	v_pk_mul_f32 v[18:19], v[36:37], v[16:17] op_sel:[1,1] op_sel_hi:[1,0] neg_lo:[1,0]
	s_nop 0
	v_pk_fma_f32 v[16:17], v[36:37], v[16:17], v[18:19] op_sel_hi:[0,1,1]
	ds_write2_b64 v13, v[20:21], v[16:17] offset0:224 offset1:240
	v_mov_b32_e32 v16, v182
	v_mov_b32_e32 v10, v176
	v_mov_b32_e32 v17, v175
	s_waitcnt lgkmcnt(0)
	s_barrier
	v_lshlrev_b32_e32 v190, 3, v16
	v_add_u32_e32 v190, 0x1000, v190
	global_load_dwordx2 v[202:203], v190, s[46:47] offset:-4096
	global_load_dwordx2 v[204:205], v190, s[46:47]
	v_add_u32_e32 v190, 0x2000, v190
	global_load_dwordx2 v[206:207], v190, s[46:47] offset:-4096
	global_load_dwordx2 v[208:209], v190, s[46:47]
	v_add_u32_e32 v190, 0x2000, v190
	global_load_dwordx2 v[210:211], v190, s[46:47] offset:-4096
	global_load_dwordx2 v[212:213], v190, s[46:47]
	v_add_u32_e32 v190, 0x2000, v190
	global_load_dwordx2 v[214:215], v190, s[46:47] offset:-4096
	global_load_dwordx2 v[216:217], v190, s[46:47]
	v_add_u32_e32 v190, 0x2000, v190
	global_load_dwordx2 v[218:219], v190, s[46:47] offset:-4096
	global_load_dwordx2 v[220:221], v190, s[46:47]
	v_add_u32_e32 v190, 0x2000, v190
	global_load_dwordx2 v[222:223], v190, s[46:47] offset:-4096
	global_load_dwordx2 v[224:225], v190, s[46:47]
	v_add_u32_e32 v190, 0x2000, v190
	global_load_dwordx2 v[226:227], v190, s[46:47] offset:-4096
	global_load_dwordx2 v[228:229], v190, s[46:47]
	v_add_u32_e32 v190, 0x2000, v190
	global_load_dwordx2 v[230:231], v190, s[46:47] offset:-4096
	global_load_dwordx2 v[232:233], v190, s[46:47]
	v_mov_b32_e32 v50, v165
	v_lshlrev_b32_e32 v13, 3, v17
	v_lshlrev_b32_e32 v48, 3, v10
	v_add3_u32 v10, 0, v13, v48
	v_xor_b32_e32 v13, 1, v17
	v_xor_b32_e32 v34, 8, v17
	v_xor_b32_e32 v36, 9, v17
	v_lshlrev_b32_e32 v13, 3, v13
	v_xor_b32_e32 v15, 2, v17
	v_xor_b32_e32 v24, 3, v17
	v_xor_b32_e32 v26, 4, v17
	v_xor_b32_e32 v28, 5, v17
	v_xor_b32_e32 v30, 6, v17
	v_xor_b32_e32 v32, 7, v17
	v_lshlrev_b32_e32 v34, 3, v34
	v_lshlrev_b32_e32 v36, 3, v36
	v_xor_b32_e32 v38, 10, v17
	v_xor_b32_e32 v40, 11, v17
	v_xor_b32_e32 v42, 12, v17
	v_xor_b32_e32 v44, 13, v17
	v_xor_b32_e32 v46, 14, v17
	v_xor_b32_e32 v17, 15, v17
	v_add3_u32 v13, 0, v13, v48
	v_lshlrev_b32_e32 v15, 3, v15
	v_lshlrev_b32_e32 v24, 3, v24
	v_lshlrev_b32_e32 v26, 3, v26
	v_lshlrev_b32_e32 v28, 3, v28
	v_lshlrev_b32_e32 v30, 3, v30
	v_lshlrev_b32_e32 v32, 3, v32
	v_add3_u32 v57, 0, v34, v48
	v_add3_u32 v58, 0, v36, v48
	v_lshlrev_b32_e32 v38, 3, v38
	v_lshlrev_b32_e32 v40, 3, v40
	v_lshlrev_b32_e32 v42, 3, v42
	v_lshlrev_b32_e32 v44, 3, v44
	v_lshlrev_b32_e32 v46, 3, v46
	v_lshlrev_b32_e32 v17, 3, v17
	ds_read_b64 v[18:19], v10
	ds_read_b64 v[20:21], v13
	v_add3_u32 v15, 0, v15, v48
	v_add3_u32 v52, 0, v24, v48
	v_add3_u32 v53, 0, v26, v48
	v_add3_u32 v54, 0, v28, v48
	v_add3_u32 v55, 0, v30, v48
	v_add3_u32 v56, 0, v32, v48
	ds_read_b64 v[34:35], v57
	ds_read_b64 v[36:37], v58
	v_add3_u32 v59, 0, v38, v48
	v_add3_u32 v60, 0, v40, v48
	v_add3_u32 v61, 0, v42, v48
	v_add3_u32 v62, 0, v44, v48
	v_add3_u32 v63, 0, v46, v48
	v_add3_u32 v64, 0, v17, v48
	v_mov_b32_e32 v17, v1
	ds_read_b64 v[22:23], v15
	ds_read_b64 v[24:25], v52
	ds_read_b64 v[26:27], v53
	ds_read_b64 v[28:29], v54
	ds_read_b64 v[30:31], v55
	ds_read_b64 v[32:33], v56
	ds_read_b64 v[38:39], v59
	ds_read_b64 v[40:41], v60
	ds_read_b64 v[42:43], v61
	ds_read_b64 v[44:45], v62
	ds_read_b64 v[46:47], v63
	ds_read_b64 v[48:49], v64
	s_waitcnt lgkmcnt(13)
	v_pk_add_f32 v[70:71], v[18:19], v[34:35]
	v_mov_b32_e32 v17, v164
	v_pk_add_f32 v[18:19], v[18:19], v[34:35] neg_lo:[0,1] neg_hi:[0,1]
	v_mov_b32_e32 v17, v166
	s_waitcnt lgkmcnt(12)
	v_pk_add_f32 v[34:35], v[20:21], v[36:37]
	v_pk_add_f32 v[20:21], v[20:21], v[36:37] neg_lo:[0,1] neg_hi:[0,1]
	v_mov_b32_e32 v66, v167
	v_mov_b32_e32 v17, v168
	v_mov_b32_e32 v68, v169
	s_nop 0
	v_pk_mul_f32 v[36:37], v[20:21], v[68:69] op_sel:[1,0] op_sel_hi:[0,0] neg_lo:[1,1] neg_hi:[0,1]
	v_mov_b32_e32 v17, v170
	v_pk_fma_f32 v[20:21], v[20:21], v[50:51], v[36:37] op_sel_hi:[1,0,1]
	s_waitcnt lgkmcnt(5)
	v_pk_add_f32 v[36:37], v[22:23], v[38:39]
	v_pk_add_f32 v[22:23], v[22:23], v[38:39] neg_lo:[0,1] neg_hi:[0,1]
	s_nop 0
	v_pk_mul_f32 v[38:39], v[22:23], v[66:67] op_sel:[1,0] op_sel_hi:[0,0] neg_lo:[1,1] neg_hi:[0,1]
	v_mov_b32_e32 v17, v171
	v_pk_fma_f32 v[22:23], v[22:23], v[66:67], v[38:39] op_sel_hi:[1,0,1]
	s_waitcnt lgkmcnt(4)
	v_pk_add_f32 v[38:39], v[24:25], v[40:41]
	v_pk_add_f32 v[24:25], v[24:25], v[40:41] neg_lo:[0,1] neg_hi:[0,1]
	s_nop 0
	v_pk_mul_f32 v[40:41], v[24:25], v[68:69] op_sel_hi:[1,0]
	s_nop 0
	v_pk_fma_f32 v[24:25], v[24:25], v[50:51], v[40:41] op_sel:[1,0,0] op_sel_hi:[0,0,1] neg_lo:[1,1,0] neg_hi:[0,1,0]
	s_waitcnt lgkmcnt(3)
	v_pk_add_f32 v[40:41], v[26:27], v[42:43]
	v_pk_add_f32 v[26:27], v[26:27], v[42:43] neg_lo:[0,1] neg_hi:[0,1]
	v_ashrrev_i32_e32 v17, 31, v16
	v_xor_b32_e32 v73, 0x80000000, v26
	v_mov_b32_e32 v72, v27
	s_waitcnt lgkmcnt(2)
	v_pk_add_f32 v[26:27], v[28:29], v[44:45]
	v_pk_add_f32 v[28:29], v[28:29], v[44:45] neg_lo:[0,1] neg_hi:[0,1]
	s_nop 0
	v_pk_mul_f32 v[42:43], v[28:29], v[68:69] op_sel_hi:[1,0] neg_lo:[0,1] neg_hi:[0,1]
	s_nop 0
	v_pk_fma_f32 v[28:29], v[28:29], v[50:51], v[42:43] op_sel:[1,0,0] op_sel_hi:[0,0,1] neg_lo:[1,1,0] neg_hi:[0,1,0]
	s_waitcnt lgkmcnt(1)
	v_pk_add_f32 v[42:43], v[30:31], v[46:47]
	v_pk_add_f32 v[30:31], v[30:31], v[46:47] neg_lo:[0,1] neg_hi:[0,1]
	s_nop 0
	v_pk_mul_f32 v[44:45], v[30:31], v[66:67] op_sel:[1,0] op_sel_hi:[0,0] neg_lo:[1,1] neg_hi:[0,1]
	s_nop 0
	v_pk_fma_f32 v[30:31], v[30:31], v[66:67], v[44:45] op_sel_hi:[1,0,1] neg_lo:[0,1,0] neg_hi:[0,1,0]
	s_waitcnt lgkmcnt(0)
	v_pk_add_f32 v[44:45], v[32:33], v[48:49]
	v_pk_add_f32 v[32:33], v[32:33], v[48:49] neg_lo:[0,1] neg_hi:[0,1]
	v_pk_add_f32 v[48:49], v[34:35], v[26:27]
	v_pk_add_f32 v[26:27], v[34:35], v[26:27] neg_lo:[0,1] neg_hi:[0,1]
	s_nop 0
	v_pk_mul_f32 v[34:35], v[26:27], v[66:67] op_sel:[1,0] op_sel_hi:[0,0] neg_lo:[1,1] neg_hi:[0,1]
	v_pk_fma_f32 v[26:27], v[26:27], v[66:67], v[34:35] op_sel_hi:[1,0,1]
	v_pk_add_f32 v[34:35], v[36:37], v[42:43]
	v_pk_add_f32 v[36:37], v[36:37], v[42:43] neg_lo:[0,1] neg_hi:[0,1]
	v_pk_mul_f32 v[46:47], v[32:33], v[68:69] op_sel:[1,0] op_sel_hi:[0,0] neg_lo:[1,1] neg_hi:[0,1]
	v_xor_b32_e32 v43, 0x80000000, v36
	v_mov_b32_e32 v42, v37
	v_pk_add_f32 v[36:37], v[38:39], v[44:45]
	v_pk_add_f32 v[38:39], v[38:39], v[44:45] neg_lo:[0,1] neg_hi:[0,1]
	v_pk_fma_f32 v[46:47], v[32:33], v[50:51], v[46:47] op_sel_hi:[1,0,1] neg_lo:[0,1,0] neg_hi:[0,1,0]
	v_pk_add_f32 v[32:33], v[70:71], v[40:41]
	v_pk_mul_f32 v[44:45], v[38:39], v[66:67] op_sel:[1,0] op_sel_hi:[0,0] neg_lo:[1,1] neg_hi:[0,1]
	v_pk_add_f32 v[40:41], v[70:71], v[40:41] neg_lo:[0,1] neg_hi:[0,1]
	v_pk_fma_f32 v[38:39], v[38:39], v[66:67], v[44:45] op_sel_hi:[1,0,1] neg_lo:[0,1,0] neg_hi:[0,1,0]
	v_pk_add_f32 v[44:45], v[32:33], v[34:35]
	v_pk_add_f32 v[32:33], v[32:33], v[34:35] neg_lo:[0,1] neg_hi:[0,1]
	v_pk_add_f32 v[34:35], v[48:49], v[36:37]
	v_pk_add_f32 v[36:37], v[48:49], v[36:37] neg_lo:[0,1] neg_hi:[0,1]
	v_pk_add_f32 v[50:51], v[44:45], v[34:35]
	v_xor_b32_e32 v49, 0x80000000, v36
	v_mov_b32_e32 v48, v37
	v_pk_add_f32 v[36:37], v[44:45], v[34:35] neg_lo:[0,1] neg_hi:[0,1]
	v_pk_add_f32 v[68:69], v[32:33], v[48:49]
	v_pk_add_f32 v[44:45], v[32:33], v[48:49] neg_lo:[0,1] neg_hi:[0,1]
	v_pk_add_f32 v[32:33], v[40:41], v[42:43]
	v_pk_add_f32 v[34:35], v[40:41], v[42:43] neg_lo:[0,1] neg_hi:[0,1]
	v_pk_add_f32 v[40:41], v[26:27], v[38:39]
	v_pk_add_f32 v[26:27], v[26:27], v[38:39] neg_lo:[0,1] neg_hi:[0,1]
	v_pk_add_f32 v[42:43], v[32:33], v[40:41] neg_lo:[0,1] neg_hi:[0,1]
	v_xor_b32_e32 v39, 0x80000000, v26
	v_mov_b32_e32 v38, v27
	v_pk_add_f32 v[26:27], v[32:33], v[40:41]
	v_pk_add_f32 v[40:41], v[20:21], v[28:29]
	v_pk_add_f32 v[20:21], v[20:21], v[28:29] neg_lo:[0,1] neg_hi:[0,1]
	v_pk_add_f32 v[32:33], v[34:35], v[38:39]
	v_pk_mul_f32 v[28:29], v[66:67], v[20:21] op_sel:[0,1] op_sel_hi:[0,0] neg_lo:[1,1] neg_hi:[1,0]
	v_pk_fma_f32 v[20:21], v[66:67], v[20:21], v[28:29] op_sel_hi:[0,1,1]
	v_pk_add_f32 v[28:29], v[22:23], v[30:31]
	v_pk_add_f32 v[22:23], v[22:23], v[30:31] neg_lo:[0,1] neg_hi:[0,1]
	v_pk_add_f32 v[38:39], v[34:35], v[38:39] neg_lo:[0,1] neg_hi:[0,1]
	v_xor_b32_e32 v31, 0x80000000, v22
	v_mov_b32_e32 v30, v23
	v_pk_add_f32 v[22:23], v[24:25], v[46:47]
	v_pk_add_f32 v[24:25], v[24:25], v[46:47] neg_lo:[0,1] neg_hi:[0,1]
	v_pk_add_f32 v[34:35], v[18:19], v[72:73]
	v_pk_mul_f32 v[46:47], v[66:67], v[24:25] op_sel:[0,1] op_sel_hi:[0,0] neg_lo:[1,1] neg_hi:[1,0]
	v_pk_fma_f32 v[24:25], v[66:67], v[24:25], v[46:47] op_sel_hi:[0,1,1] neg_lo:[1,0,0] neg_hi:[1,0,0]
	v_pk_add_f32 v[46:47], v[34:35], v[28:29]
	v_pk_add_f32 v[28:29], v[34:35], v[28:29] neg_lo:[0,1] neg_hi:[0,1]
	v_pk_add_f32 v[34:35], v[40:41], v[22:23]
	v_pk_add_f32 v[22:23], v[40:41], v[22:23] neg_lo:[0,1] neg_hi:[0,1]
	v_pk_add_f32 v[18:19], v[18:19], v[72:73] neg_lo:[0,1] neg_hi:[0,1]
	v_pk_add_f32 v[66:67], v[28:29], v[22:23] op_sel:[0,1] op_sel_hi:[1,0] neg_hi:[0,1]
	v_pk_add_f32 v[48:49], v[28:29], v[22:23] op_sel:[0,1] op_sel_hi:[1,0] neg_lo:[0,1]
	v_pk_add_f32 v[28:29], v[18:19], v[30:31]
	v_pk_add_f32 v[18:19], v[18:19], v[30:31] neg_lo:[0,1] neg_hi:[0,1]
	v_pk_add_f32 v[30:31], v[20:21], v[24:25]
	v_pk_add_f32 v[20:21], v[20:21], v[24:25] neg_lo:[0,1] neg_hi:[0,1]
	v_pk_add_f32 v[22:23], v[46:47], v[34:35]
	v_xor_b32_e32 v25, 0x80000000, v20
	v_mov_b32_e32 v24, v21
	v_lshl_add_u64 v[20:21], v[16:17], 3, s[46:47]
	s_waitcnt vmcnt(0)
	v_pk_add_f32 v[40:41], v[46:47], v[34:35] neg_lo:[0,1] neg_hi:[0,1]
	v_pk_add_f32 v[34:35], v[18:19], v[24:25]
	v_pk_add_f32 v[18:19], v[18:19], v[24:25] neg_lo:[0,1] neg_hi:[0,1]
	v_pk_add_f32 v[70:71], v[28:29], v[30:31]
	v_pk_add_f32 v[46:47], v[28:29], v[30:31] neg_lo:[0,1] neg_hi:[0,1]
	v_mov_b32_e32 v17, v1
	s_nop 0
	v_pk_mul_f32 v[24:25], v[50:51], v[202:203] op_sel:[1,1] op_sel_hi:[1,0] neg_lo:[1,0]
	s_nop 0
	v_pk_fma_f32 v[20:21], v[50:51], v[202:203], v[24:25] op_sel_hi:[0,1,1]
	v_add_u32_e32 v24, 0x200, v16
	v_ashrrev_i32_e32 v25, 31, v24
	v_lshl_add_u64 v[24:25], v[24:25], 3, s[46:47]
	s_nop 0
	v_pk_mul_f32 v[28:29], v[204:205], v[22:23] op_sel:[1,1] op_sel_hi:[0,1] neg_lo:[0,1]
	v_pk_fma_f32 v[22:23], v[204:205], v[22:23], v[28:29] op_sel_hi:[1,0,1]
	v_add_u32_e32 v24, 0x400, v16
	v_ashrrev_i32_e32 v25, 31, v24
	v_lshl_add_u64 v[24:25], v[24:25], 3, s[46:47]
	s_nop 0
	v_pk_mul_f32 v[28:29], v[26:27], v[206:207] op_sel:[1,1] op_sel_hi:[1,0] neg_lo:[1,0]
	s_nop 0
	v_pk_fma_f32 v[24:25], v[26:27], v[206:207], v[28:29] op_sel_hi:[0,1,1]
	v_add_u32_e32 v26, 0x600, v16
	v_ashrrev_i32_e32 v27, 31, v26
	v_lshl_add_u64 v[26:27], v[26:27], 3, s[46:47]
	s_nop 0
	v_pk_mul_f32 v[28:29], v[208:209], v[70:71] op_sel:[1,1] op_sel_hi:[0,1] neg_lo:[0,1]
	v_pk_fma_f32 v[26:27], v[208:209], v[70:71], v[28:29] op_sel_hi:[1,0,1]
	v_add_u32_e32 v28, 0x800, v16
	v_ashrrev_i32_e32 v29, 31, v28
	v_lshl_add_u64 v[28:29], v[28:29], 3, s[46:47]
	s_nop 0
	v_pk_mul_f32 v[30:31], v[68:69], v[210:211] op_sel:[1,1] op_sel_hi:[1,0] neg_lo:[1,0]
	s_nop 0
	v_pk_fma_f32 v[28:29], v[68:69], v[210:211], v[30:31] op_sel_hi:[0,1,1]
	v_add_u32_e32 v30, 0xa00, v16
	v_ashrrev_i32_e32 v31, 31, v30
	v_lshl_add_u64 v[30:31], v[30:31], 3, s[46:47]
	v_mov_b32_e32 v68, v169
	s_nop 0
	v_pk_mul_f32 v[50:51], v[212:213], v[66:67] op_sel:[1,1] op_sel_hi:[0,1] neg_lo:[0,1]
	v_pk_fma_f32 v[30:31], v[212:213], v[66:67], v[50:51] op_sel_hi:[1,0,1]
	v_add_u32_e32 v50, 0xc00, v16
	v_ashrrev_i32_e32 v51, 31, v50
	v_lshl_add_u64 v[50:51], v[50:51], 3, s[46:47]
	s_nop 0
	v_pk_mul_f32 v[66:67], v[32:33], v[214:215] op_sel:[1,1] op_sel_hi:[1,0] neg_lo:[1,0]
	s_nop 0
	v_pk_fma_f32 v[32:33], v[32:33], v[214:215], v[66:67] op_sel_hi:[0,1,1]
	v_add_u32_e32 v50, 0xe00, v16
	v_ashrrev_i32_e32 v51, 31, v50
	v_lshl_add_u64 v[50:51], v[50:51], 3, s[46:47]
	s_nop 0
	v_pk_mul_f32 v[66:67], v[216:217], v[34:35] op_sel:[1,1] op_sel_hi:[0,1] neg_lo:[0,1]
	v_pk_fma_f32 v[34:35], v[216:217], v[34:35], v[66:67] op_sel_hi:[1,0,1]
	v_add_u32_e32 v50, 0x1000, v16
	v_ashrrev_i32_e32 v51, 31, v50
	v_lshl_add_u64 v[50:51], v[50:51], 3, s[46:47]
	s_nop 0
	v_pk_mul_f32 v[66:67], v[36:37], v[218:219] op_sel:[1,1] op_sel_hi:[1,0] neg_lo:[1,0]
	s_nop 0
	v_pk_fma_f32 v[36:37], v[36:37], v[218:219], v[66:67] op_sel_hi:[0,1,1]
	v_add_u32_e32 v50, 0x1200, v16
	v_ashrrev_i32_e32 v51, 31, v50
	v_lshl_add_u64 v[50:51], v[50:51], 3, s[46:47]
	v_pk_add_f32 v[70:71], v[20:21], v[36:37]
	v_pk_add_f32 v[20:21], v[20:21], v[36:37] neg_lo:[0,1] neg_hi:[0,1]
	s_nop 0
	v_pk_mul_f32 v[66:67], v[40:41], v[220:221] op_sel:[1,1] op_sel_hi:[1,0] neg_lo:[1,0]
	s_nop 0
	v_pk_fma_f32 v[40:41], v[40:41], v[220:221], v[66:67] op_sel_hi:[0,1,1]
	v_add_u32_e32 v50, 0x1400, v16
	v_ashrrev_i32_e32 v51, 31, v50
	v_lshl_add_u64 v[50:51], v[50:51], 3, s[46:47]
	v_pk_add_f32 v[36:37], v[22:23], v[40:41]
	v_pk_add_f32 v[22:23], v[22:23], v[40:41] neg_lo:[0,1] neg_hi:[0,1]
	s_nop 0
	v_pk_mul_f32 v[66:67], v[42:43], v[222:223] op_sel:[1,1] op_sel_hi:[1,0] neg_lo:[1,0]
	s_nop 0
	v_pk_fma_f32 v[42:43], v[42:43], v[222:223], v[66:67] op_sel_hi:[0,1,1]
	v_add_u32_e32 v50, 0x1600, v16
	v_ashrrev_i32_e32 v51, 31, v50
	v_lshl_add_u64 v[50:51], v[50:51], 3, s[46:47]
	s_nop 0
	v_pk_mul_f32 v[66:67], v[46:47], v[224:225] op_sel:[1,1] op_sel_hi:[1,0] neg_lo:[1,0]
	s_nop 0
	v_pk_fma_f32 v[46:47], v[46:47], v[224:225], v[66:67] op_sel_hi:[0,1,1]
	v_add_u32_e32 v50, 0x1800, v16
	v_ashrrev_i32_e32 v51, 31, v50
	v_lshl_add_u64 v[50:51], v[50:51], 3, s[46:47]
	s_nop 0
	v_pk_mul_f32 v[66:67], v[44:45], v[226:227] op_sel:[1,1] op_sel_hi:[1,0] neg_lo:[1,0]
	s_nop 0
	v_pk_fma_f32 v[44:45], v[44:45], v[226:227], v[66:67] op_sel_hi:[0,1,1]
	v_add_u32_e32 v50, 0x1a00, v16
	v_ashrrev_i32_e32 v51, 31, v50
	v_lshl_add_u64 v[50:51], v[50:51], 3, s[46:47]
	s_nop 0
	v_pk_mul_f32 v[66:67], v[48:49], v[228:229] op_sel:[1,1] op_sel_hi:[1,0] neg_lo:[1,0]
	s_nop 0
	v_pk_fma_f32 v[48:49], v[48:49], v[228:229], v[66:67] op_sel_hi:[0,1,1]
	v_add_u32_e32 v50, 0x1c00, v16
	v_ashrrev_i32_e32 v51, 31, v50
	v_lshl_add_u64 v[50:51], v[50:51], 3, s[46:47]
	s_nop 0
	v_pk_mul_f32 v[66:67], v[38:39], v[230:231] op_sel:[1,1] op_sel_hi:[1,0] neg_lo:[1,0]
	s_nop 0
	v_pk_fma_f32 v[38:39], v[38:39], v[230:231], v[66:67] op_sel_hi:[0,1,1]
	v_add_u32_e32 v50, 0x1e00, v16
	v_ashrrev_i32_e32 v51, 31, v50
	v_lshl_add_u64 v[50:51], v[50:51], 3, s[46:47]
	v_mov_b32_e32 v50, v232
	v_mov_b32_e32 v51, v233
	v_lshlrev_b32_e32 v190, 3, v16
	v_add_u32_e32 v190, 0x11000, v190
	global_load_dwordx2 v[202:203], v190, s[46:47] offset:-4096
	global_load_dwordx2 v[204:205], v190, s[46:47]
	v_add_u32_e32 v190, 0x2000, v190
	global_load_dwordx2 v[206:207], v190, s[46:47] offset:-4096
	global_load_dwordx2 v[208:209], v190, s[46:47]
	v_add_u32_e32 v190, 0x2000, v190
	global_load_dwordx2 v[210:211], v190, s[46:47] offset:-4096
	global_load_dwordx2 v[212:213], v190, s[46:47]
	v_add_u32_e32 v190, 0x2000, v190
	global_load_dwordx2 v[214:215], v190, s[46:47] offset:-4096
	global_load_dwordx2 v[216:217], v190, s[46:47]
	v_add_u32_e32 v190, 0x2000, v190
	global_load_dwordx2 v[218:219], v190, s[46:47] offset:-4096
	global_load_dwordx2 v[220:221], v190, s[46:47]
	v_add_u32_e32 v190, 0x2000, v190
	global_load_dwordx2 v[222:223], v190, s[46:47] offset:-4096
	global_load_dwordx2 v[224:225], v190, s[46:47]
	v_add_u32_e32 v190, 0x2000, v190
	global_load_dwordx2 v[226:227], v190, s[46:47] offset:-4096
	global_load_dwordx2 v[228:229], v190, s[46:47]
	v_add_u32_e32 v190, 0x2000, v190
	global_load_dwordx2 v[230:231], v190, s[46:47] offset:-4096
	global_load_dwordx2 v[232:233], v190, s[46:47]
	v_mov_b32_e32 v17, v164
	s_nop 0
	v_pk_mul_f32 v[66:67], v[18:19], v[50:51] op_sel:[1,1] op_sel_hi:[1,0] neg_lo:[1,0]
	s_nop 0
	v_pk_fma_f32 v[18:19], v[18:19], v[50:51], v[66:67] op_sel_hi:[0,1,1]
	v_mov_b32_e32 v50, v165
	v_mov_b32_e32 v17, v166
	v_mov_b32_e32 v66, v167
	v_mov_b32_e32 v17, v168
	s_nop 0
	v_pk_mul_f32 v[40:41], v[22:23], v[68:69] op_sel:[1,0] op_sel_hi:[0,0] neg_lo:[1,0]
	v_mov_b32_e32 v17, v170
	v_pk_fma_f32 v[22:23], v[22:23], v[50:51], v[40:41] op_sel_hi:[1,0,1]
	v_pk_add_f32 v[40:41], v[24:25], v[42:43]
	v_pk_add_f32 v[24:25], v[24:25], v[42:43] neg_lo:[0,1] neg_hi:[0,1]
	s_nop 0
	v_pk_mul_f32 v[42:43], v[24:25], v[66:67] op_sel:[1,0] op_sel_hi:[0,0] neg_lo:[1,0]
	v_mov_b32_e32 v17, v171
	v_pk_fma_f32 v[24:25], v[24:25], v[66:67], v[42:43] op_sel_hi:[1,0,1]
	v_pk_add_f32 v[42:43], v[26:27], v[46:47]
	v_pk_add_f32 v[26:27], v[26:27], v[46:47] neg_lo:[0,1] neg_hi:[0,1]
	s_nop 0
	v_pk_mul_f32 v[46:47], v[26:27], v[68:69] op_sel_hi:[1,0]
	s_nop 0
	v_pk_fma_f32 v[26:27], v[26:27], v[50:51], v[46:47] op_sel:[1,0,0] op_sel_hi:[0,0,1] neg_lo:[1,0,0]
	v_pk_add_f32 v[46:47], v[28:29], v[44:45]
	v_pk_add_f32 v[28:29], v[28:29], v[44:45] neg_lo:[0,1] neg_hi:[0,1]
	v_mov_b32_e32 v17, v175
	v_xor_b32_e32 v44, 0x80000000, v29
	v_mov_b32_e32 v45, v28
	v_pk_add_f32 v[28:29], v[30:31], v[48:49]
	v_pk_add_f32 v[30:31], v[30:31], v[48:49] neg_lo:[0,1] neg_hi:[0,1]
	s_nop 0
	v_pk_mul_f32 v[48:49], v[30:31], v[68:69] op_sel_hi:[1,0] neg_lo:[0,1] neg_hi:[0,1]
	s_nop 0
	v_pk_fma_f32 v[30:31], v[30:31], v[50:51], v[48:49] op_sel:[1,0,0] op_sel_hi:[0,0,1] neg_lo:[1,0,0]
	v_pk_add_f32 v[48:49], v[32:33], v[38:39]
	v_pk_add_f32 v[32:33], v[32:33], v[38:39] neg_lo:[0,1] neg_hi:[0,1]
	s_nop 0
	v_pk_mul_f32 v[38:39], v[32:33], v[66:67] op_sel:[1,0] op_sel_hi:[0,0] neg_lo:[1,0]
	s_nop 0
	v_pk_fma_f32 v[32:33], v[32:33], v[66:67], v[38:39] op_sel_hi:[1,0,1] neg_lo:[0,1,0] neg_hi:[0,1,0]
	v_pk_add_f32 v[38:39], v[34:35], v[18:19]
	v_pk_add_f32 v[18:19], v[34:35], v[18:19] neg_lo:[0,1] neg_hi:[0,1]
	s_nop 0
	v_pk_mul_f32 v[34:35], v[18:19], v[68:69] op_sel:[1,0] op_sel_hi:[0,0] neg_lo:[1,0]
	v_mov_b32_e32 v68, v169
	v_pk_fma_f32 v[18:19], v[18:19], v[50:51], v[34:35] op_sel_hi:[1,0,1] neg_lo:[0,1,0] neg_hi:[0,1,0]
	v_pk_add_f32 v[50:51], v[36:37], v[28:29]
	v_pk_add_f32 v[28:29], v[36:37], v[28:29] neg_lo:[0,1] neg_hi:[0,1]
	v_pk_add_f32 v[34:35], v[70:71], v[46:47]
	v_pk_mul_f32 v[36:37], v[28:29], v[66:67] op_sel:[1,0] op_sel_hi:[0,0] neg_lo:[1,0]
	v_pk_add_f32 v[46:47], v[70:71], v[46:47] neg_lo:[0,1] neg_hi:[0,1]
	v_pk_fma_f32 v[28:29], v[28:29], v[66:67], v[36:37] op_sel_hi:[1,0,1]
	v_pk_add_f32 v[36:37], v[40:41], v[48:49]
	v_pk_add_f32 v[40:41], v[40:41], v[48:49] neg_lo:[0,1] neg_hi:[0,1]
	s_nop 0
	v_xor_b32_e32 v48, 0x80000000, v41
	v_mov_b32_e32 v49, v40
	v_pk_add_f32 v[40:41], v[42:43], v[38:39]
	v_pk_add_f32 v[38:39], v[42:43], v[38:39] neg_lo:[0,1] neg_hi:[0,1]
	s_nop 0
	v_pk_mul_f32 v[42:43], v[66:67], v[38:39] op_sel:[0,1] op_sel_hi:[0,0] neg_lo:[0,1]
	v_pk_fma_f32 v[38:39], v[38:39], v[66:67], v[42:43] op_sel_hi:[1,0,1] neg_lo:[0,1,0] neg_hi:[0,1,0]
	v_pk_add_f32 v[42:43], v[34:35], v[36:37]
	v_pk_add_f32 v[34:35], v[34:35], v[36:37] neg_lo:[0,1] neg_hi:[0,1]
	v_pk_add_f32 v[36:37], v[50:51], v[40:41]
	v_pk_add_f32 v[40:41], v[50:51], v[40:41] neg_lo:[0,1] neg_hi:[0,1]
	s_nop 0
	v_xor_b32_e32 v50, 0x80000000, v41
	v_mov_b32_e32 v51, v40
	v_pk_add_f32 v[40:41], v[42:43], v[36:37]
	v_pk_add_f32 v[36:37], v[42:43], v[36:37] neg_lo:[0,1] neg_hi:[0,1]
	v_pk_add_f32 v[42:43], v[34:35], v[50:51]
	v_pk_add_f32 v[34:35], v[34:35], v[50:51] neg_lo:[0,1] neg_hi:[0,1]
	v_pk_add_f32 v[50:51], v[46:47], v[48:49]
	v_pk_add_f32 v[46:47], v[46:47], v[48:49] neg_lo:[0,1] neg_hi:[0,1]
	v_pk_add_f32 v[48:49], v[28:29], v[38:39]
	v_pk_add_f32 v[28:29], v[28:29], v[38:39] neg_lo:[0,1] neg_hi:[0,1]
	s_nop 0
	v_xor_b32_e32 v38, 0x80000000, v29
	v_mov_b32_e32 v39, v28
	v_pk_add_f32 v[28:29], v[50:51], v[48:49]
	v_pk_add_f32 v[48:49], v[50:51], v[48:49] neg_lo:[0,1] neg_hi:[0,1]
	v_pk_add_f32 v[50:51], v[46:47], v[38:39]
	v_pk_add_f32 v[38:39], v[46:47], v[38:39] neg_lo:[0,1] neg_hi:[0,1]
	v_pk_add_f32 v[46:47], v[20:21], v[44:45]
	v_pk_add_f32 v[20:21], v[20:21], v[44:45] neg_lo:[0,1] neg_hi:[0,1]
	v_pk_add_f32 v[44:45], v[22:23], v[30:31]
	v_pk_add_f32 v[22:23], v[22:23], v[30:31] neg_lo:[0,1] neg_hi:[0,1]
	s_nop 0
	v_pk_mul_f32 v[30:31], v[66:67], v[22:23] op_sel:[0,1] op_sel_hi:[0,0] neg_lo:[0,1]
	v_pk_fma_f32 v[22:23], v[66:67], v[22:23], v[30:31] op_sel_hi:[0,1,1]
	v_pk_add_f32 v[30:31], v[24:25], v[32:33]
	v_pk_add_f32 v[24:25], v[24:25], v[32:33] neg_lo:[0,1] neg_hi:[0,1]
	s_nop 0
	v_xor_b32_e32 v32, 0x80000000, v25
	v_mov_b32_e32 v33, v24
	v_pk_add_f32 v[24:25], v[26:27], v[18:19]
	v_pk_add_f32 v[18:19], v[26:27], v[18:19] neg_lo:[0,1] neg_hi:[0,1]
	s_nop 0
	v_pk_mul_f32 v[26:27], v[66:67], v[18:19] op_sel:[0,1] op_sel_hi:[0,0] neg_lo:[0,1]
	v_pk_fma_f32 v[18:19], v[66:67], v[18:19], v[26:27] op_sel_hi:[0,1,1] neg_lo:[1,0,0] neg_hi:[1,0,0]
	v_pk_add_f32 v[26:27], v[46:47], v[30:31]
	v_pk_add_f32 v[30:31], v[46:47], v[30:31] neg_lo:[0,1] neg_hi:[0,1]
	v_pk_add_f32 v[46:47], v[44:45], v[24:25]
	v_pk_add_f32 v[24:25], v[44:45], v[24:25] neg_lo:[0,1] neg_hi:[0,1]
	v_mov_b32_e32 v66, v167
	v_xor_b32_e32 v44, 0x80000000, v25
	v_mov_b32_e32 v45, v24
	v_pk_add_f32 v[24:25], v[26:27], v[46:47]
	v_pk_add_f32 v[26:27], v[26:27], v[46:47] neg_lo:[0,1] neg_hi:[0,1]
	v_pk_add_f32 v[46:47], v[30:31], v[44:45]
	v_pk_add_f32 v[30:31], v[30:31], v[44:45] neg_lo:[0,1] neg_hi:[0,1]
	v_pk_add_f32 v[44:45], v[20:21], v[32:33]
	v_pk_add_f32 v[20:21], v[20:21], v[32:33] neg_lo:[0,1] neg_hi:[0,1]
	v_pk_add_f32 v[32:33], v[22:23], v[18:19]
	v_pk_add_f32 v[18:19], v[22:23], v[18:19] neg_lo:[0,1] neg_hi:[0,1]
	s_nop 0
	v_xor_b32_e32 v22, 0x80000000, v19
	v_mov_b32_e32 v23, v18
	v_pk_add_f32 v[18:19], v[44:45], v[32:33]
	v_pk_add_f32 v[32:33], v[44:45], v[32:33] neg_lo:[0,1] neg_hi:[0,1]
	v_pk_add_f32 v[44:45], v[20:21], v[22:23]
	v_pk_add_f32 v[20:21], v[20:21], v[22:23] neg_lo:[0,1] neg_hi:[0,1]
	ds_write_b64 v10, v[40:41]
	ds_write_b64 v13, v[24:25]
	ds_write_b64 v15, v[28:29]
	ds_write_b64 v52, v[18:19]
	ds_write_b64 v53, v[42:43]
	ds_write_b64 v54, v[46:47]
	ds_write_b64 v55, v[50:51]
	ds_write_b64 v56, v[44:45]
	ds_write_b64 v57, v[36:37]
	ds_write_b64 v58, v[26:27]
	ds_write_b64 v59, v[48:49]
	ds_write_b64 v60, v[32:33]
	ds_write_b64 v61, v[34:35]
	ds_write_b64 v62, v[30:31]
	ds_write_b64 v63, v[38:39]
	ds_write_b64 v64, v[20:21]
	v_mov_b32_e32 v10, v177
	v_mov_b32_e32 v64, v165
	v_lshlrev_b32_e32 v13, 3, v17
	v_lshlrev_b32_e32 v48, 3, v10
	v_add3_u32 v10, 0, v13, v48
	v_xor_b32_e32 v13, 1, v17
	v_xor_b32_e32 v34, 8, v17
	v_xor_b32_e32 v36, 9, v17
	v_lshlrev_b32_e32 v13, 3, v13
	v_xor_b32_e32 v15, 2, v17
	v_xor_b32_e32 v24, 3, v17
	v_xor_b32_e32 v26, 4, v17
	v_xor_b32_e32 v28, 5, v17
	v_xor_b32_e32 v30, 6, v17
	v_xor_b32_e32 v32, 7, v17
	v_lshlrev_b32_e32 v34, 3, v34
	v_lshlrev_b32_e32 v36, 3, v36
	v_xor_b32_e32 v38, 10, v17
	v_xor_b32_e32 v40, 11, v17
	v_xor_b32_e32 v42, 12, v17
	v_xor_b32_e32 v44, 13, v17
	v_xor_b32_e32 v46, 14, v17
	v_xor_b32_e32 v17, 15, v17
	v_add3_u32 v13, 0, v13, v48
	v_lshlrev_b32_e32 v15, 3, v15
	v_lshlrev_b32_e32 v24, 3, v24
	v_lshlrev_b32_e32 v26, 3, v26
	v_lshlrev_b32_e32 v28, 3, v28
	v_lshlrev_b32_e32 v30, 3, v30
	v_lshlrev_b32_e32 v32, 3, v32
	v_add3_u32 v55, 0, v34, v48
	v_add3_u32 v56, 0, v36, v48
	v_lshlrev_b32_e32 v38, 3, v38
	v_lshlrev_b32_e32 v40, 3, v40
	v_lshlrev_b32_e32 v42, 3, v42
	v_lshlrev_b32_e32 v44, 3, v44
	v_lshlrev_b32_e32 v46, 3, v46
	v_lshlrev_b32_e32 v17, 3, v17
	ds_read_b64 v[18:19], v10
	ds_read_b64 v[20:21], v13
	v_add3_u32 v15, 0, v15, v48
	v_add3_u32 v50, 0, v24, v48
	v_add3_u32 v51, 0, v26, v48
	v_add3_u32 v52, 0, v28, v48
	v_add3_u32 v53, 0, v30, v48
	v_add3_u32 v54, 0, v32, v48
	ds_read_b64 v[34:35], v55
	ds_read_b64 v[36:37], v56
	v_add3_u32 v57, 0, v38, v48
	v_add3_u32 v58, 0, v40, v48
	v_add3_u32 v59, 0, v42, v48
	v_add3_u32 v60, 0, v44, v48
	v_add3_u32 v61, 0, v46, v48
	v_add3_u32 v62, 0, v17, v48
	v_mov_b32_e32 v17, v1
	ds_read_b64 v[22:23], v15
	ds_read_b64 v[24:25], v50
	ds_read_b64 v[26:27], v51
	ds_read_b64 v[28:29], v52
	ds_read_b64 v[30:31], v53
	ds_read_b64 v[32:33], v54
	ds_read_b64 v[38:39], v57
	ds_read_b64 v[40:41], v58
	ds_read_b64 v[42:43], v59
	ds_read_b64 v[44:45], v60
	ds_read_b64 v[46:47], v61
	ds_read_b64 v[48:49], v62
	s_waitcnt lgkmcnt(13)
	v_pk_add_f32 v[70:71], v[18:19], v[34:35]
	v_mov_b32_e32 v17, v164
	v_pk_add_f32 v[18:19], v[18:19], v[34:35] neg_lo:[0,1] neg_hi:[0,1]
	v_mov_b32_e32 v17, v166
	s_waitcnt lgkmcnt(12)
	v_pk_add_f32 v[34:35], v[20:21], v[36:37]
	v_pk_add_f32 v[20:21], v[20:21], v[36:37] neg_lo:[0,1] neg_hi:[0,1]
	v_mov_b32_e32 v17, v168
	s_nop 0
	v_pk_mul_f32 v[36:37], v[20:21], v[68:69] op_sel:[1,0] op_sel_hi:[0,0] neg_lo:[1,1] neg_hi:[0,1]
	v_mov_b32_e32 v17, v170
	v_pk_fma_f32 v[20:21], v[20:21], v[64:65], v[36:37] op_sel_hi:[1,0,1]
	s_waitcnt lgkmcnt(5)
	v_pk_add_f32 v[36:37], v[22:23], v[38:39]
	v_pk_add_f32 v[22:23], v[22:23], v[38:39] neg_lo:[0,1] neg_hi:[0,1]
	s_nop 0
	v_pk_mul_f32 v[38:39], v[22:23], v[66:67] op_sel:[1,0] op_sel_hi:[0,0] neg_lo:[1,1] neg_hi:[0,1]
	v_mov_b32_e32 v17, v171
	v_pk_fma_f32 v[22:23], v[22:23], v[66:67], v[38:39] op_sel_hi:[1,0,1]
	s_waitcnt lgkmcnt(4)
	v_pk_add_f32 v[38:39], v[24:25], v[40:41]
	v_pk_add_f32 v[24:25], v[24:25], v[40:41] neg_lo:[0,1] neg_hi:[0,1]
	s_nop 0
	v_pk_mul_f32 v[40:41], v[24:25], v[68:69] op_sel_hi:[1,0]
	s_nop 0
	v_pk_fma_f32 v[24:25], v[24:25], v[64:65], v[40:41] op_sel:[1,0,0] op_sel_hi:[0,0,1] neg_lo:[1,1,0] neg_hi:[0,1,0]
	s_waitcnt lgkmcnt(3)
	v_pk_add_f32 v[40:41], v[26:27], v[42:43]
	v_pk_add_f32 v[26:27], v[26:27], v[42:43] neg_lo:[0,1] neg_hi:[0,1]
	s_nop 0
	v_xor_b32_e32 v73, 0x80000000, v26
	v_mov_b32_e32 v72, v27
	s_waitcnt lgkmcnt(2)
	v_pk_add_f32 v[26:27], v[28:29], v[44:45]
	v_pk_add_f32 v[28:29], v[28:29], v[44:45] neg_lo:[0,1] neg_hi:[0,1]
	s_nop 0
	v_pk_mul_f32 v[42:43], v[28:29], v[68:69] op_sel_hi:[1,0] neg_lo:[0,1] neg_hi:[0,1]
	s_nop 0
	v_pk_fma_f32 v[28:29], v[28:29], v[64:65], v[42:43] op_sel:[1,0,0] op_sel_hi:[0,0,1] neg_lo:[1,1,0] neg_hi:[0,1,0]
	s_waitcnt lgkmcnt(1)
	v_pk_add_f32 v[42:43], v[30:31], v[46:47]
	v_pk_add_f32 v[30:31], v[30:31], v[46:47] neg_lo:[0,1] neg_hi:[0,1]
	s_nop 0
	v_pk_mul_f32 v[44:45], v[30:31], v[66:67] op_sel:[1,0] op_sel_hi:[0,0] neg_lo:[1,1] neg_hi:[0,1]
	s_nop 0
	v_pk_fma_f32 v[30:31], v[30:31], v[66:67], v[44:45] op_sel_hi:[1,0,1] neg_lo:[0,1,0] neg_hi:[0,1,0]
	s_waitcnt lgkmcnt(0)
	v_pk_add_f32 v[44:45], v[32:33], v[48:49]
	v_pk_add_f32 v[32:33], v[32:33], v[48:49] neg_lo:[0,1] neg_hi:[0,1]
	v_pk_add_f32 v[48:49], v[34:35], v[26:27]
	v_pk_add_f32 v[26:27], v[34:35], v[26:27] neg_lo:[0,1] neg_hi:[0,1]
	s_nop 0
	v_pk_mul_f32 v[34:35], v[26:27], v[66:67] op_sel:[1,0] op_sel_hi:[0,0] neg_lo:[1,1] neg_hi:[0,1]
	v_pk_fma_f32 v[26:27], v[26:27], v[66:67], v[34:35] op_sel_hi:[1,0,1]
	v_pk_add_f32 v[34:35], v[36:37], v[42:43]
	v_pk_add_f32 v[36:37], v[36:37], v[42:43] neg_lo:[0,1] neg_hi:[0,1]
	v_pk_mul_f32 v[46:47], v[32:33], v[68:69] op_sel:[1,0] op_sel_hi:[0,0] neg_lo:[1,1] neg_hi:[0,1]
	v_xor_b32_e32 v43, 0x80000000, v36
	v_mov_b32_e32 v42, v37
	v_pk_add_f32 v[36:37], v[38:39], v[44:45]
	v_pk_add_f32 v[38:39], v[38:39], v[44:45] neg_lo:[0,1] neg_hi:[0,1]
	v_pk_fma_f32 v[46:47], v[32:33], v[64:65], v[46:47] op_sel_hi:[1,0,1] neg_lo:[0,1,0] neg_hi:[0,1,0]
	v_pk_add_f32 v[32:33], v[70:71], v[40:41]
	v_pk_mul_f32 v[44:45], v[38:39], v[66:67] op_sel:[1,0] op_sel_hi:[0,0] neg_lo:[1,1] neg_hi:[0,1]
	v_pk_add_f32 v[40:41], v[70:71], v[40:41] neg_lo:[0,1] neg_hi:[0,1]
	v_pk_fma_f32 v[38:39], v[38:39], v[66:67], v[44:45] op_sel_hi:[1,0,1] neg_lo:[0,1,0] neg_hi:[0,1,0]
	v_pk_add_f32 v[44:45], v[32:33], v[34:35]
	v_pk_add_f32 v[32:33], v[32:33], v[34:35] neg_lo:[0,1] neg_hi:[0,1]
	v_pk_add_f32 v[34:35], v[48:49], v[36:37]
	v_pk_add_f32 v[36:37], v[48:49], v[36:37] neg_lo:[0,1] neg_hi:[0,1]
	v_pk_add_f32 v[64:65], v[44:45], v[34:35]
	v_xor_b32_e32 v49, 0x80000000, v36
	v_mov_b32_e32 v48, v37
	v_pk_add_f32 v[36:37], v[44:45], v[34:35] neg_lo:[0,1] neg_hi:[0,1]
	v_pk_add_f32 v[68:69], v[32:33], v[48:49]
	v_pk_add_f32 v[44:45], v[32:33], v[48:49] neg_lo:[0,1] neg_hi:[0,1]
	v_pk_add_f32 v[32:33], v[40:41], v[42:43]
	v_pk_add_f32 v[34:35], v[40:41], v[42:43] neg_lo:[0,1] neg_hi:[0,1]
	v_pk_add_f32 v[40:41], v[26:27], v[38:39]
	v_pk_add_f32 v[26:27], v[26:27], v[38:39] neg_lo:[0,1] neg_hi:[0,1]
	v_pk_add_f32 v[42:43], v[32:33], v[40:41] neg_lo:[0,1] neg_hi:[0,1]
	v_xor_b32_e32 v39, 0x80000000, v26
	v_mov_b32_e32 v38, v27
	v_pk_add_f32 v[26:27], v[32:33], v[40:41]
	v_pk_add_f32 v[40:41], v[20:21], v[28:29]
	v_pk_add_f32 v[20:21], v[20:21], v[28:29] neg_lo:[0,1] neg_hi:[0,1]
	v_pk_add_f32 v[32:33], v[34:35], v[38:39]
	v_pk_mul_f32 v[28:29], v[66:67], v[20:21] op_sel:[0,1] op_sel_hi:[0,0] neg_lo:[1,1] neg_hi:[1,0]
	v_pk_fma_f32 v[20:21], v[66:67], v[20:21], v[28:29] op_sel_hi:[0,1,1]
	v_pk_add_f32 v[28:29], v[22:23], v[30:31]
	v_pk_add_f32 v[22:23], v[22:23], v[30:31] neg_lo:[0,1] neg_hi:[0,1]
	v_pk_add_f32 v[38:39], v[34:35], v[38:39] neg_lo:[0,1] neg_hi:[0,1]
	v_xor_b32_e32 v31, 0x80000000, v22
	v_mov_b32_e32 v30, v23
	v_pk_add_f32 v[22:23], v[24:25], v[46:47]
	v_pk_add_f32 v[24:25], v[24:25], v[46:47] neg_lo:[0,1] neg_hi:[0,1]
	v_pk_add_f32 v[34:35], v[18:19], v[72:73]
	v_pk_mul_f32 v[46:47], v[66:67], v[24:25] op_sel:[0,1] op_sel_hi:[0,0] neg_lo:[1,1] neg_hi:[1,0]
	v_pk_fma_f32 v[24:25], v[66:67], v[24:25], v[46:47] op_sel_hi:[0,1,1] neg_lo:[1,0,0] neg_hi:[1,0,0]
	v_pk_add_f32 v[46:47], v[34:35], v[28:29]
	v_pk_add_f32 v[28:29], v[34:35], v[28:29] neg_lo:[0,1] neg_hi:[0,1]
	v_pk_add_f32 v[34:35], v[40:41], v[22:23]
	v_pk_add_f32 v[22:23], v[40:41], v[22:23] neg_lo:[0,1] neg_hi:[0,1]
	v_pk_add_f32 v[18:19], v[18:19], v[72:73] neg_lo:[0,1] neg_hi:[0,1]
	v_pk_add_f32 v[66:67], v[28:29], v[22:23] op_sel:[0,1] op_sel_hi:[1,0] neg_hi:[0,1]
	v_pk_add_f32 v[48:49], v[28:29], v[22:23] op_sel:[0,1] op_sel_hi:[1,0] neg_lo:[0,1]
	v_pk_add_f32 v[28:29], v[18:19], v[30:31]
	v_pk_add_f32 v[18:19], v[18:19], v[30:31] neg_lo:[0,1] neg_hi:[0,1]
	v_pk_add_f32 v[30:31], v[20:21], v[24:25]
	v_pk_add_f32 v[20:21], v[20:21], v[24:25] neg_lo:[0,1] neg_hi:[0,1]
	v_pk_add_f32 v[22:23], v[46:47], v[34:35]
	v_xor_b32_e32 v25, 0x80000000, v20
	v_add_u32_e32 v20, 0x2000, v16
	v_mov_b32_e32 v24, v21
	v_ashrrev_i32_e32 v21, 31, v20
	v_lshl_add_u64 v[20:21], v[20:21], 3, s[46:47]
	s_waitcnt vmcnt(0)
	v_pk_add_f32 v[40:41], v[46:47], v[34:35] neg_lo:[0,1] neg_hi:[0,1]
	v_pk_add_f32 v[34:35], v[18:19], v[24:25]
	v_pk_add_f32 v[18:19], v[18:19], v[24:25] neg_lo:[0,1] neg_hi:[0,1]
	v_pk_add_f32 v[70:71], v[28:29], v[30:31]
	v_pk_add_f32 v[46:47], v[28:29], v[30:31] neg_lo:[0,1] neg_hi:[0,1]
	s_nop 0
	v_pk_mul_f32 v[24:25], v[64:65], v[202:203] op_sel:[1,1] op_sel_hi:[1,0] neg_lo:[1,0]
	s_nop 0
	v_pk_fma_f32 v[20:21], v[64:65], v[202:203], v[24:25] op_sel_hi:[0,1,1]
	v_add_u32_e32 v24, 0x2200, v16
	v_ashrrev_i32_e32 v25, 31, v24
	v_lshl_add_u64 v[24:25], v[24:25], 3, s[46:47]
	s_nop 0
	v_pk_mul_f32 v[28:29], v[204:205], v[22:23] op_sel:[1,1] op_sel_hi:[0,1] neg_lo:[0,1]
	v_pk_fma_f32 v[22:23], v[204:205], v[22:23], v[28:29] op_sel_hi:[1,0,1]
	v_add_u32_e32 v24, 0x2400, v16
	v_ashrrev_i32_e32 v25, 31, v24
	v_lshl_add_u64 v[24:25], v[24:25], 3, s[46:47]
	s_nop 0
	v_pk_mul_f32 v[28:29], v[26:27], v[206:207] op_sel:[1,1] op_sel_hi:[1,0] neg_lo:[1,0]
	s_nop 0
	v_pk_fma_f32 v[24:25], v[26:27], v[206:207], v[28:29] op_sel_hi:[0,1,1]
	v_add_u32_e32 v26, 0x2600, v16
	v_ashrrev_i32_e32 v27, 31, v26
	v_lshl_add_u64 v[26:27], v[26:27], 3, s[46:47]
	s_nop 0
	v_pk_mul_f32 v[28:29], v[208:209], v[70:71] op_sel:[1,1] op_sel_hi:[0,1] neg_lo:[0,1]
	v_pk_fma_f32 v[26:27], v[208:209], v[70:71], v[28:29] op_sel_hi:[1,0,1]
	v_add_u32_e32 v28, 0x2800, v16
	v_ashrrev_i32_e32 v29, 31, v28
	v_lshl_add_u64 v[28:29], v[28:29], 3, s[46:47]
	s_nop 0
	v_pk_mul_f32 v[30:31], v[68:69], v[210:211] op_sel:[1,1] op_sel_hi:[1,0] neg_lo:[1,0]
	s_nop 0
	v_pk_fma_f32 v[28:29], v[68:69], v[210:211], v[30:31] op_sel_hi:[0,1,1]
	v_add_u32_e32 v30, 0x2a00, v16
	v_ashrrev_i32_e32 v31, 31, v30
	v_lshl_add_u64 v[30:31], v[30:31], 3, s[46:47]
	s_nop 0
	v_pk_mul_f32 v[64:65], v[212:213], v[66:67] op_sel:[1,1] op_sel_hi:[0,1] neg_lo:[0,1]
	v_pk_fma_f32 v[30:31], v[212:213], v[66:67], v[64:65] op_sel_hi:[1,0,1]
	v_add_u32_e32 v64, 0x2c00, v16
	v_ashrrev_i32_e32 v65, 31, v64
	v_lshl_add_u64 v[64:65], v[64:65], 3, s[46:47]
	s_nop 0
	v_pk_mul_f32 v[66:67], v[32:33], v[214:215] op_sel:[1,1] op_sel_hi:[1,0] neg_lo:[1,0]
	s_nop 0
	v_pk_fma_f32 v[32:33], v[32:33], v[214:215], v[66:67] op_sel_hi:[0,1,1]
	v_add_u32_e32 v64, 0x2e00, v16
	v_ashrrev_i32_e32 v65, 31, v64
	v_lshl_add_u64 v[64:65], v[64:65], 3, s[46:47]
	s_nop 0
	v_pk_mul_f32 v[66:67], v[216:217], v[34:35] op_sel:[1,1] op_sel_hi:[0,1] neg_lo:[0,1]
	v_pk_fma_f32 v[34:35], v[216:217], v[34:35], v[66:67] op_sel_hi:[1,0,1]
	v_add_u32_e32 v64, 0x3000, v16
	v_ashrrev_i32_e32 v65, 31, v64
	v_lshl_add_u64 v[64:65], v[64:65], 3, s[46:47]
	s_nop 0
	v_pk_mul_f32 v[66:67], v[36:37], v[218:219] op_sel:[1,1] op_sel_hi:[1,0] neg_lo:[1,0]
	s_nop 0
	v_pk_fma_f32 v[36:37], v[36:37], v[218:219], v[66:67] op_sel_hi:[0,1,1]
	v_add_u32_e32 v64, 0x3200, v16
	v_ashrrev_i32_e32 v65, 31, v64
	v_lshl_add_u64 v[64:65], v[64:65], 3, s[46:47]
	v_pk_add_f32 v[68:69], v[20:21], v[36:37]
	v_pk_add_f32 v[20:21], v[20:21], v[36:37] neg_lo:[0,1] neg_hi:[0,1]
	s_nop 0
	v_pk_mul_f32 v[66:67], v[40:41], v[220:221] op_sel:[1,1] op_sel_hi:[1,0] neg_lo:[1,0]
	s_nop 0
	v_pk_fma_f32 v[40:41], v[40:41], v[220:221], v[66:67] op_sel_hi:[0,1,1]
	v_add_u32_e32 v64, 0x3400, v16
	v_ashrrev_i32_e32 v65, 31, v64
	v_lshl_add_u64 v[64:65], v[64:65], 3, s[46:47]
	v_pk_add_f32 v[36:37], v[22:23], v[40:41]
	v_pk_add_f32 v[22:23], v[22:23], v[40:41] neg_lo:[0,1] neg_hi:[0,1]
	s_nop 0
	v_pk_mul_f32 v[66:67], v[42:43], v[222:223] op_sel:[1,1] op_sel_hi:[1,0] neg_lo:[1,0]
	s_nop 0
	v_pk_fma_f32 v[42:43], v[42:43], v[222:223], v[66:67] op_sel_hi:[0,1,1]
	v_add_u32_e32 v64, 0x3600, v16
	v_ashrrev_i32_e32 v65, 31, v64
	v_lshl_add_u64 v[64:65], v[64:65], 3, s[46:47]
	s_nop 0
	v_pk_mul_f32 v[66:67], v[46:47], v[224:225] op_sel:[1,1] op_sel_hi:[1,0] neg_lo:[1,0]
	s_nop 0
	v_pk_fma_f32 v[46:47], v[46:47], v[224:225], v[66:67] op_sel_hi:[0,1,1]
	v_add_u32_e32 v64, 0x3800, v16
	v_ashrrev_i32_e32 v65, 31, v64
	v_lshl_add_u64 v[64:65], v[64:65], 3, s[46:47]
	s_nop 0
	v_pk_mul_f32 v[66:67], v[44:45], v[226:227] op_sel:[1,1] op_sel_hi:[1,0] neg_lo:[1,0]
	s_nop 0
	v_pk_fma_f32 v[44:45], v[44:45], v[226:227], v[66:67] op_sel_hi:[0,1,1]
	v_add_u32_e32 v64, 0x3a00, v16
	v_ashrrev_i32_e32 v65, 31, v64
	v_lshl_add_u64 v[64:65], v[64:65], 3, s[46:47]
	s_nop 0
	v_pk_mul_f32 v[66:67], v[48:49], v[228:229] op_sel:[1,1] op_sel_hi:[1,0] neg_lo:[1,0]
	s_nop 0
	v_pk_fma_f32 v[48:49], v[48:49], v[228:229], v[66:67] op_sel_hi:[0,1,1]
	v_add_u32_e32 v64, 0x3c00, v16
	v_ashrrev_i32_e32 v65, 31, v64
	v_lshl_add_u64 v[64:65], v[64:65], 3, s[46:47]
	v_add_u32_e32 v16, 0x3e00, v16
	v_ashrrev_i32_e32 v17, 31, v16
	v_lshl_add_u64 v[16:17], v[16:17], 3, s[46:47]
	s_nop 0
	v_pk_mul_f32 v[66:67], v[38:39], v[230:231] op_sel:[1,1] op_sel_hi:[1,0] neg_lo:[1,0]
	s_nop 0
	v_pk_fma_f32 v[38:39], v[38:39], v[230:231], v[66:67] op_sel_hi:[0,1,1]
	s_nop 0
	v_pk_mul_f32 v[64:65], v[18:19], v[232:233] op_sel:[1,1] op_sel_hi:[1,0] neg_lo:[1,0]
	v_mov_b32_e32 v66, v169
	v_pk_fma_f32 v[16:17], v[18:19], v[232:233], v[64:65] op_sel_hi:[0,1,1]
	v_mov_b32_e32 v18, v1
	v_mov_b32_e32 v19, v166
	v_mov_b32_e32 v18, v164
	v_mov_b32_e32 v64, v167
	v_mov_b32_e32 v18, v165
	s_nop 0
	v_mov_b32_e32 v19, v168
	s_nop 0
	v_mov_b32_e32 v19, v170
	v_pk_mul_f32 v[40:41], v[22:23], v[66:67] op_sel:[1,0] op_sel_hi:[0,0] neg_lo:[1,0]
	v_mov_b32_e32 v19, v171
	s_nop 0
	v_pk_fma_f32 v[22:23], v[22:23], v[18:19], v[40:41] op_sel_hi:[1,0,1]
	v_pk_add_f32 v[40:41], v[24:25], v[42:43]
	v_pk_add_f32 v[24:25], v[24:25], v[42:43] neg_lo:[0,1] neg_hi:[0,1]
	s_nop 0
	v_pk_mul_f32 v[42:43], v[24:25], v[64:65] op_sel:[1,0] op_sel_hi:[0,0] neg_lo:[1,0]
	s_nop 0
	v_pk_fma_f32 v[24:25], v[24:25], v[64:65], v[42:43] op_sel_hi:[1,0,1]
	v_pk_add_f32 v[42:43], v[26:27], v[46:47]
	v_pk_add_f32 v[26:27], v[26:27], v[46:47] neg_lo:[0,1] neg_hi:[0,1]
	s_nop 0
	v_pk_mul_f32 v[46:47], v[26:27], v[66:67] op_sel_hi:[1,0]
	s_nop 0
	v_pk_fma_f32 v[26:27], v[26:27], v[18:19], v[46:47] op_sel:[1,0,0] op_sel_hi:[0,0,1] neg_lo:[1,0,0]
	v_pk_add_f32 v[46:47], v[28:29], v[44:45]
	v_pk_add_f32 v[28:29], v[28:29], v[44:45] neg_lo:[0,1] neg_hi:[0,1]
	s_nop 0
	v_xor_b32_e32 v44, 0x80000000, v29
	v_mov_b32_e32 v45, v28
	v_pk_add_f32 v[28:29], v[30:31], v[48:49]
	v_pk_add_f32 v[30:31], v[30:31], v[48:49] neg_lo:[0,1] neg_hi:[0,1]
	s_nop 0
	v_pk_mul_f32 v[48:49], v[30:31], v[66:67] op_sel_hi:[1,0] neg_lo:[0,1] neg_hi:[0,1]
	s_nop 0
	v_pk_fma_f32 v[30:31], v[30:31], v[18:19], v[48:49] op_sel:[1,0,0] op_sel_hi:[0,0,1] neg_lo:[1,0,0]
	v_pk_add_f32 v[48:49], v[32:33], v[38:39]
	v_pk_add_f32 v[32:33], v[32:33], v[38:39] neg_lo:[0,1] neg_hi:[0,1]
	s_nop 0
	v_pk_mul_f32 v[38:39], v[32:33], v[64:65] op_sel:[1,0] op_sel_hi:[0,0] neg_lo:[1,0]
	s_nop 0
	v_pk_fma_f32 v[32:33], v[32:33], v[64:65], v[38:39] op_sel_hi:[1,0,1] neg_lo:[0,1,0] neg_hi:[0,1,0]
	v_pk_add_f32 v[38:39], v[34:35], v[16:17]
	v_pk_add_f32 v[16:17], v[34:35], v[16:17] neg_lo:[0,1] neg_hi:[0,1]
	s_nop 0
	v_pk_mul_f32 v[34:35], v[16:17], v[66:67] op_sel:[1,0] op_sel_hi:[0,0] neg_lo:[1,0]
	s_nop 0
	v_pk_fma_f32 v[16:17], v[16:17], v[18:19], v[34:35] op_sel_hi:[1,0,1] neg_lo:[0,1,0] neg_hi:[0,1,0]
	v_pk_add_f32 v[18:19], v[68:69], v[46:47]
	v_pk_add_f32 v[34:35], v[68:69], v[46:47] neg_lo:[0,1] neg_hi:[0,1]
	v_pk_add_f32 v[46:47], v[36:37], v[28:29]
	v_pk_add_f32 v[28:29], v[36:37], v[28:29] neg_lo:[0,1] neg_hi:[0,1]
	s_nop 0
	v_pk_mul_f32 v[36:37], v[28:29], v[64:65] op_sel:[1,0] op_sel_hi:[0,0] neg_lo:[1,0]
	s_nop 0
	v_pk_fma_f32 v[28:29], v[28:29], v[64:65], v[36:37] op_sel_hi:[1,0,1]
	v_pk_add_f32 v[36:37], v[40:41], v[48:49]
	v_pk_add_f32 v[40:41], v[40:41], v[48:49] neg_lo:[0,1] neg_hi:[0,1]
	s_nop 0
	v_xor_b32_e32 v48, 0x80000000, v41
	v_mov_b32_e32 v49, v40
	v_pk_add_f32 v[40:41], v[42:43], v[38:39]
	v_pk_add_f32 v[38:39], v[42:43], v[38:39] neg_lo:[0,1] neg_hi:[0,1]
	s_nop 0
	v_pk_mul_f32 v[42:43], v[64:65], v[38:39] op_sel:[0,1] op_sel_hi:[0,0] neg_lo:[0,1]
	v_pk_fma_f32 v[38:39], v[38:39], v[64:65], v[42:43] op_sel_hi:[1,0,1] neg_lo:[0,1,0] neg_hi:[0,1,0]
	v_pk_add_f32 v[42:43], v[18:19], v[36:37]
	v_pk_add_f32 v[18:19], v[18:19], v[36:37] neg_lo:[0,1] neg_hi:[0,1]
	v_pk_add_f32 v[36:37], v[46:47], v[40:41]
	v_pk_add_f32 v[40:41], v[46:47], v[40:41] neg_lo:[0,1] neg_hi:[0,1]
	s_nop 0
	v_xor_b32_e32 v46, 0x80000000, v41
	v_mov_b32_e32 v47, v40
	v_pk_add_f32 v[40:41], v[42:43], v[36:37]
	v_pk_add_f32 v[36:37], v[42:43], v[36:37] neg_lo:[0,1] neg_hi:[0,1]
	v_pk_add_f32 v[42:43], v[18:19], v[46:47]
	v_pk_add_f32 v[18:19], v[18:19], v[46:47] neg_lo:[0,1] neg_hi:[0,1]
	v_pk_add_f32 v[46:47], v[34:35], v[48:49]
	v_pk_add_f32 v[34:35], v[34:35], v[48:49] neg_lo:[0,1] neg_hi:[0,1]
	v_pk_add_f32 v[48:49], v[28:29], v[38:39]
	v_pk_add_f32 v[28:29], v[28:29], v[38:39] neg_lo:[0,1] neg_hi:[0,1]
	s_nop 0
	v_xor_b32_e32 v38, 0x80000000, v29
	v_mov_b32_e32 v39, v28
	v_pk_add_f32 v[28:29], v[46:47], v[48:49]
	v_pk_add_f32 v[46:47], v[46:47], v[48:49] neg_lo:[0,1] neg_hi:[0,1]
	v_pk_add_f32 v[48:49], v[34:35], v[38:39]
	v_pk_add_f32 v[34:35], v[34:35], v[38:39] neg_lo:[0,1] neg_hi:[0,1]
	v_pk_add_f32 v[38:39], v[20:21], v[44:45]
	v_pk_add_f32 v[20:21], v[20:21], v[44:45] neg_lo:[0,1] neg_hi:[0,1]
	v_pk_add_f32 v[44:45], v[22:23], v[30:31]
	v_pk_add_f32 v[22:23], v[22:23], v[30:31] neg_lo:[0,1] neg_hi:[0,1]
	s_nop 0
	v_pk_mul_f32 v[30:31], v[64:65], v[22:23] op_sel:[0,1] op_sel_hi:[0,0] neg_lo:[0,1]
	v_pk_fma_f32 v[22:23], v[64:65], v[22:23], v[30:31] op_sel_hi:[0,1,1]
	v_pk_add_f32 v[30:31], v[24:25], v[32:33]
	v_pk_add_f32 v[24:25], v[24:25], v[32:33] neg_lo:[0,1] neg_hi:[0,1]
	s_nop 0
	v_xor_b32_e32 v32, 0x80000000, v25
	v_mov_b32_e32 v33, v24
	v_pk_add_f32 v[24:25], v[26:27], v[16:17]
	v_pk_add_f32 v[16:17], v[26:27], v[16:17] neg_lo:[0,1] neg_hi:[0,1]
	s_nop 0
	v_pk_mul_f32 v[26:27], v[64:65], v[16:17] op_sel:[0,1] op_sel_hi:[0,0] neg_lo:[0,1]
	v_pk_fma_f32 v[16:17], v[64:65], v[16:17], v[26:27] op_sel_hi:[0,1,1] neg_lo:[1,0,0] neg_hi:[1,0,0]
	v_pk_add_f32 v[26:27], v[38:39], v[30:31]
	v_pk_add_f32 v[30:31], v[38:39], v[30:31] neg_lo:[0,1] neg_hi:[0,1]
	v_pk_add_f32 v[38:39], v[44:45], v[24:25]
	v_pk_add_f32 v[24:25], v[44:45], v[24:25] neg_lo:[0,1] neg_hi:[0,1]
	s_nop 0
	v_xor_b32_e32 v44, 0x80000000, v25
	v_mov_b32_e32 v45, v24
	v_pk_add_f32 v[24:25], v[26:27], v[38:39]
	v_pk_add_f32 v[26:27], v[26:27], v[38:39] neg_lo:[0,1] neg_hi:[0,1]
	v_pk_add_f32 v[38:39], v[30:31], v[44:45]
	v_pk_add_f32 v[30:31], v[30:31], v[44:45] neg_lo:[0,1] neg_hi:[0,1]
	v_pk_add_f32 v[44:45], v[20:21], v[32:33]
	v_pk_add_f32 v[20:21], v[20:21], v[32:33] neg_lo:[0,1] neg_hi:[0,1]
	v_pk_add_f32 v[32:33], v[22:23], v[16:17]
	v_pk_add_f32 v[16:17], v[22:23], v[16:17] neg_lo:[0,1] neg_hi:[0,1]
	s_nop 0
	v_xor_b32_e32 v22, 0x80000000, v17
	v_mov_b32_e32 v23, v16
	v_pk_add_f32 v[16:17], v[44:45], v[32:33]
	v_pk_add_f32 v[32:33], v[44:45], v[32:33] neg_lo:[0,1] neg_hi:[0,1]
	v_pk_add_f32 v[44:45], v[20:21], v[22:23]
	v_pk_add_f32 v[20:21], v[20:21], v[22:23] neg_lo:[0,1] neg_hi:[0,1]
	ds_write_b64 v10, v[40:41]
	ds_write_b64 v13, v[24:25]
	ds_write_b64 v15, v[28:29]
	ds_write_b64 v50, v[16:17]
	ds_write_b64 v51, v[42:43]
	ds_write_b64 v52, v[38:39]
	ds_write_b64 v53, v[48:49]
	ds_write_b64 v54, v[44:45]
	ds_write_b64 v55, v[36:37]
	ds_write_b64 v56, v[26:27]
	ds_write_b64 v57, v[46:47]
	ds_write_b64 v58, v[32:33]
	ds_write_b64 v59, v[18:19]
	ds_write_b64 v60, v[30:31]
	ds_write_b64 v61, v[34:35]
	ds_write_b64 v62, v[20:21]
	v_mov_b32_e32 v10, v174
	v_mov_b32_e32 v50, v172
	s_waitcnt lgkmcnt(0)
	s_barrier
	v_add_u32_e32 v13, v50, v10
	v_lshl_add_u32 v13, v13, 3, 0
	ds_read2_b64 v[16:19], v13 offset1:16
	v_xad_u32 v15, v50, 1, v10
	v_lshl_add_u32 v15, v15, 3, 0
	s_waitcnt lgkmcnt(0)
	v_pk_fma_f32 v[16:17], v[16:17], 0, v[16:17] op_sel:[1,0,0] op_sel_hi:[0,0,1] neg_hi:[1,0,0]
	v_pk_fma_f32 v[22:23], v[180:181], s[90:91], v[180:181] op_sel:[1,0,0] op_sel_hi:[0,1,1]
	v_pk_mul_f32 v[24:25], v[22:23], v[18:19] op_sel:[1,1] op_sel_hi:[1,0] neg_hi:[0,1]
	s_nop 0
	v_pk_fma_f32 v[18:19], v[18:19], v[22:23], v[24:25] op_sel_hi:[1,0,1]
	v_pk_mul_f32 v[24:25], v[180:181], v[22:23] op_sel:[1,1] op_sel_hi:[0,1] neg_lo:[0,1]
	v_pk_fma_f32 v[26:27], v[180:181], v[22:23], v[24:25] op_sel_hi:[1,0,1]
	ds_read2_b64 v[22:25], v15 offset0:32 offset1:48
	s_waitcnt lgkmcnt(0)
	v_pk_mul_f32 v[28:29], v[22:23], v[26:27] op_sel:[1,1] op_sel_hi:[0,1] neg_hi:[1,0]
	s_nop 0
	v_pk_fma_f32 v[22:23], v[22:23], v[26:27], v[28:29] op_sel_hi:[1,0,1]
	v_pk_mul_f32 v[28:29], v[180:181], v[26:27] op_sel:[1,1] op_sel_hi:[0,1] neg_lo:[0,1]
	v_pk_fma_f32 v[26:27], v[180:181], v[26:27], v[28:29] op_sel_hi:[1,0,1]
	s_nop 0
	v_pk_mul_f32 v[28:29], v[24:25], v[26:27] op_sel:[1,1] op_sel_hi:[0,1] neg_hi:[1,0]
	s_nop 0
	v_pk_fma_f32 v[24:25], v[24:25], v[26:27], v[28:29] op_sel_hi:[1,0,1]
	v_pk_mul_f32 v[28:29], v[180:181], v[26:27] op_sel:[1,1] op_sel_hi:[0,1] neg_lo:[0,1]
	v_pk_fma_f32 v[26:27], v[180:181], v[26:27], v[28:29] op_sel_hi:[1,0,1]
	v_xad_u32 v28, v50, 2, v10
	v_lshl_add_u32 v51, v28, 3, 0
	ds_read2_b64 v[28:31], v51 offset0:64 offset1:80
	v_pk_mul_f32 v[32:33], v[180:181], v[26:27] op_sel:[1,1] op_sel_hi:[0,1] neg_lo:[0,1]
	s_waitcnt lgkmcnt(0)
	v_pk_mul_f32 v[34:35], v[28:29], v[26:27] op_sel:[1,1] op_sel_hi:[0,1] neg_hi:[1,0]
	s_nop 0
	v_pk_fma_f32 v[28:29], v[28:29], v[26:27], v[34:35] op_sel_hi:[1,0,1]
	v_pk_fma_f32 v[34:35], v[180:181], v[26:27], v[32:33] op_sel_hi:[1,0,1]
	s_nop 0
	v_pk_mul_f32 v[26:27], v[30:31], v[34:35] op_sel:[1,1] op_sel_hi:[0,1] neg_hi:[1,0]
	v_pk_fma_f32 v[26:27], v[30:31], v[34:35], v[26:27] op_sel_hi:[1,0,1]
	v_xad_u32 v30, v50, 3, v10
	v_lshl_add_u32 v54, v30, 3, 0
	ds_read2_b64 v[30:33], v54 offset0:96 offset1:112
	v_pk_mul_f32 v[36:37], v[180:181], v[34:35] op_sel:[1,1] op_sel_hi:[0,1] neg_lo:[0,1]
	v_pk_fma_f32 v[34:35], v[180:181], v[34:35], v[36:37] op_sel_hi:[1,0,1]
	s_waitcnt lgkmcnt(0)
	v_pk_mul_f32 v[36:37], v[30:31], v[34:35] op_sel:[1,1] op_sel_hi:[0,1] neg_hi:[1,0]
	s_nop 0
	v_pk_fma_f32 v[30:31], v[30:31], v[34:35], v[36:37] op_sel_hi:[1,0,1]
	v_pk_mul_f32 v[36:37], v[180:181], v[34:35] op_sel:[1,1] op_sel_hi:[0,1] neg_lo:[0,1]
	v_pk_fma_f32 v[34:35], v[180:181], v[34:35], v[36:37] op_sel_hi:[1,0,1]
	s_nop 0
	v_pk_mul_f32 v[36:37], v[32:33], v[34:35] op_sel:[1,1] op_sel_hi:[0,1] neg_hi:[1,0]
	s_nop 0
	v_pk_fma_f32 v[32:33], v[32:33], v[34:35], v[36:37] op_sel_hi:[1,0,1]
	v_pk_mul_f32 v[36:37], v[180:181], v[34:35] op_sel:[1,1] op_sel_hi:[0,1] neg_lo:[0,1]
	v_pk_fma_f32 v[38:39], v[180:181], v[34:35], v[36:37] op_sel_hi:[1,0,1]
	v_xad_u32 v34, v50, 4, v10
	v_lshl_add_u32 v55, v34, 3, 0
	ds_read2_b64 v[34:37], v55 offset0:128 offset1:144
	v_pk_mul_f32 v[40:41], v[180:181], v[38:39] op_sel:[1,1] op_sel_hi:[0,1] neg_lo:[0,1]
	s_waitcnt lgkmcnt(0)
	v_pk_mul_f32 v[42:43], v[34:35], v[38:39] op_sel:[1,1] op_sel_hi:[0,1] neg_hi:[1,0]
	s_nop 0
	v_pk_fma_f32 v[34:35], v[34:35], v[38:39], v[42:43] op_sel_hi:[1,0,1]
	v_pk_fma_f32 v[42:43], v[180:181], v[38:39], v[40:41] op_sel_hi:[1,0,1]
	s_nop 0
	v_pk_mul_f32 v[38:39], v[36:37], v[42:43] op_sel:[1,1] op_sel_hi:[0,1] neg_hi:[1,0]
	v_pk_fma_f32 v[36:37], v[36:37], v[42:43], v[38:39] op_sel_hi:[1,0,1]
	v_xad_u32 v38, v50, 5, v10
	v_lshl_add_u32 v56, v38, 3, 0
	ds_read2_b64 v[38:41], v56 offset0:160 offset1:176
	v_pk_mul_f32 v[44:45], v[180:181], v[42:43] op_sel:[1,1] op_sel_hi:[0,1] neg_lo:[0,1]
	v_pk_fma_f32 v[42:43], v[180:181], v[42:43], v[44:45] op_sel_hi:[1,0,1]
	s_waitcnt lgkmcnt(0)
	v_pk_mul_f32 v[44:45], v[38:39], v[42:43] op_sel:[1,1] op_sel_hi:[0,1] neg_hi:[1,0]
	s_nop 0
	v_pk_fma_f32 v[38:39], v[38:39], v[42:43], v[44:45] op_sel_hi:[1,0,1]
	v_pk_mul_f32 v[44:45], v[180:181], v[42:43] op_sel:[1,1] op_sel_hi:[0,1] neg_lo:[0,1]
	v_pk_fma_f32 v[42:43], v[180:181], v[42:43], v[44:45] op_sel_hi:[1,0,1]
	s_nop 0
	v_pk_mul_f32 v[44:45], v[40:41], v[42:43] op_sel:[1,1] op_sel_hi:[0,1] neg_hi:[1,0]
	s_nop 0
	v_pk_fma_f32 v[40:41], v[40:41], v[42:43], v[44:45] op_sel_hi:[1,0,1]
	v_pk_mul_f32 v[44:45], v[180:181], v[42:43] op_sel:[1,1] op_sel_hi:[0,1] neg_lo:[0,1]
	v_pk_fma_f32 v[42:43], v[180:181], v[42:43], v[44:45] op_sel_hi:[1,0,1]
	v_xad_u32 v44, v50, 6, v10
	v_lshl_add_u32 v57, v44, 3, 0
	ds_read2_b64 v[44:47], v57 offset0:192 offset1:208
	v_pk_mul_f32 v[48:49], v[180:181], v[42:43] op_sel:[1,1] op_sel_hi:[0,1] neg_lo:[0,1]
	s_waitcnt lgkmcnt(0)
	v_pk_mul_f32 v[52:53], v[44:45], v[42:43] op_sel:[1,1] op_sel_hi:[0,1] neg_hi:[1,0]
	s_nop 0
	v_pk_fma_f32 v[44:45], v[44:45], v[42:43], v[52:53] op_sel_hi:[1,0,1]
	v_pk_fma_f32 v[52:53], v[180:181], v[42:43], v[48:49] op_sel_hi:[1,0,1]
	s_nop 0
	v_pk_mul_f32 v[42:43], v[46:47], v[52:53] op_sel:[1,1] op_sel_hi:[0,1] neg_hi:[1,0]
	v_pk_fma_f32 v[42:43], v[46:47], v[52:53], v[42:43] op_sel_hi:[1,0,1]
	v_xad_u32 v46, v50, 7, v10
	v_lshl_add_u32 v58, v46, 3, 0
	ds_read2_b64 v[46:49], v58 offset0:224 offset1:240
	v_pk_mul_f32 v[60:61], v[180:181], v[52:53] op_sel:[1,1] op_sel_hi:[0,1] neg_lo:[0,1]
	v_pk_fma_f32 v[52:53], v[180:181], v[52:53], v[60:61] op_sel_hi:[1,0,1]
	s_waitcnt lgkmcnt(0)
	v_pk_mul_f32 v[60:61], v[46:47], v[52:53] op_sel:[1,1] op_sel_hi:[0,1] neg_hi:[1,0]
	s_nop 0
	v_pk_fma_f32 v[46:47], v[46:47], v[52:53], v[60:61] op_sel_hi:[1,0,1]
	v_pk_mul_f32 v[60:61], v[180:181], v[52:53] op_sel:[1,1] op_sel_hi:[0,1] neg_lo:[0,1]
	v_pk_fma_f32 v[52:53], v[180:181], v[52:53], v[60:61] op_sel_hi:[1,0,1]
	s_nop 0
	v_pk_mul_f32 v[60:61], v[48:49], v[52:53] op_sel:[1,1] op_sel_hi:[0,1] neg_hi:[1,0]
	s_nop 0
	v_pk_fma_f32 v[48:49], v[48:49], v[52:53], v[60:61] op_sel_hi:[1,0,1]
	v_pk_mul_f32 v[60:61], v[180:181], v[52:53] op_sel:[1,1] op_sel_hi:[0,1] neg_lo:[0,1]
	v_pk_fma_f32 v[64:65], v[180:181], v[52:53], v[60:61] op_sel_hi:[1,0,1]
	v_xad_u32 v52, v50, 8, v10
	v_lshl_add_u32 v52, v52, 3, 0
	v_add_u32_e32 v59, 0x800, v52
	ds_read2_b64 v[60:63], v59 offset1:16
	v_pk_mul_f32 v[66:67], v[180:181], v[64:65] op_sel:[1,1] op_sel_hi:[0,1] neg_lo:[0,1]
	v_pk_fma_f32 v[66:67], v[180:181], v[64:65], v[66:67] op_sel_hi:[1,0,1]
	s_waitcnt lgkmcnt(0)
	v_pk_mul_f32 v[52:53], v[60:61], v[64:65] op_sel:[1,1] op_sel_hi:[0,1] neg_hi:[1,0]
	v_pk_fma_f32 v[52:53], v[60:61], v[64:65], v[52:53] op_sel_hi:[1,0,1]
	v_pk_mul_f32 v[60:61], v[62:63], v[66:67] op_sel:[1,1] op_sel_hi:[0,1] neg_hi:[1,0]
	v_pk_fma_f32 v[70:71], v[62:63], v[66:67], v[60:61] op_sel_hi:[1,0,1]
	v_xad_u32 v60, v50, 9, v10
	v_lshl_add_u32 v60, v60, 3, 0
	v_add_u32_e32 v60, 0x800, v60
	ds_read2_b64 v[62:65], v60 offset0:32 offset1:48
	v_pk_mul_f32 v[68:69], v[180:181], v[66:67] op_sel:[1,1] op_sel_hi:[0,1] neg_lo:[0,1]
	v_pk_fma_f32 v[66:67], v[180:181], v[66:67], v[68:69] op_sel_hi:[1,0,1]
	s_waitcnt lgkmcnt(0)
	v_pk_mul_f32 v[68:69], v[62:63], v[66:67] op_sel:[1,1] op_sel_hi:[0,1] neg_hi:[1,0]
	s_nop 0
	v_pk_fma_f32 v[72:73], v[62:63], v[66:67], v[68:69] op_sel_hi:[1,0,1]
	v_pk_mul_f32 v[62:63], v[180:181], v[66:67] op_sel:[1,1] op_sel_hi:[0,1] neg_lo:[0,1]
	v_pk_fma_f32 v[62:63], v[180:181], v[66:67], v[62:63] op_sel_hi:[1,0,1]
	s_nop 0
	v_pk_mul_f32 v[66:67], v[64:65], v[62:63] op_sel:[1,1] op_sel_hi:[0,1] neg_hi:[1,0]
	s_nop 0
	v_pk_fma_f32 v[74:75], v[64:65], v[62:63], v[66:67] op_sel_hi:[1,0,1]
	v_pk_mul_f32 v[64:65], v[180:181], v[62:63] op_sel:[1,1] op_sel_hi:[0,1] neg_lo:[0,1]
	v_pk_fma_f32 v[66:67], v[180:181], v[62:63], v[64:65] op_sel_hi:[1,0,1]
	v_xad_u32 v61, v50, 10, v10
	v_lshl_add_u32 v61, v61, 3, 0
	v_add_u32_e32 v61, 0x800, v61
	ds_read2_b64 v[62:65], v61 offset0:64 offset1:80
	v_pk_mul_f32 v[68:69], v[180:181], v[66:67] op_sel:[1,1] op_sel_hi:[0,1] neg_lo:[0,1]
	v_pk_fma_f32 v[68:69], v[180:181], v[66:67], v[68:69] op_sel_hi:[1,0,1]
	s_waitcnt lgkmcnt(0)
	v_pk_mul_f32 v[76:77], v[62:63], v[66:67] op_sel:[1,1] op_sel_hi:[0,1] neg_hi:[1,0]
	v_pk_fma_f32 v[76:77], v[62:63], v[66:67], v[76:77] op_sel_hi:[1,0,1]
	v_pk_mul_f32 v[62:63], v[64:65], v[68:69] op_sel:[1,1] op_sel_hi:[0,1] neg_hi:[1,0]
	v_pk_fma_f32 v[78:79], v[64:65], v[68:69], v[62:63] op_sel_hi:[1,0,1]
	v_xad_u32 v62, v50, 11, v10
	v_lshl_add_u32 v62, v62, 3, 0
	v_add_u32_e32 v62, 0x800, v62
	ds_read2_b64 v[64:67], v62 offset0:96 offset1:112
	v_pk_mul_f32 v[80:81], v[180:181], v[68:69] op_sel:[1,1] op_sel_hi:[0,1] neg_lo:[0,1]
	v_pk_fma_f32 v[68:69], v[180:181], v[68:69], v[80:81] op_sel_hi:[1,0,1]
	s_waitcnt lgkmcnt(0)
	v_pk_mul_f32 v[80:81], v[64:65], v[68:69] op_sel:[1,1] op_sel_hi:[0,1] neg_hi:[1,0]
	s_nop 0
	v_pk_fma_f32 v[80:81], v[64:65], v[68:69], v[80:81] op_sel_hi:[1,0,1]
	v_pk_mul_f32 v[64:65], v[180:181], v[68:69] op_sel:[1,1] op_sel_hi:[0,1] neg_lo:[0,1]
	v_pk_fma_f32 v[64:65], v[180:181], v[68:69], v[64:65] op_sel_hi:[1,0,1]
	s_nop 0
	v_pk_mul_f32 v[68:69], v[66:67], v[64:65] op_sel:[1,1] op_sel_hi:[0,1] neg_hi:[1,0]
	s_nop 0
	v_pk_fma_f32 v[82:83], v[66:67], v[64:65], v[68:69] op_sel_hi:[1,0,1]
	v_pk_mul_f32 v[66:67], v[180:181], v[64:65] op_sel:[1,1] op_sel_hi:[0,1] neg_lo:[0,1]
	v_pk_fma_f32 v[68:69], v[180:181], v[64:65], v[66:67] op_sel_hi:[1,0,1]
	v_xad_u32 v63, v50, 12, v10
	v_lshl_add_u32 v63, v63, 3, 0
	v_add_u32_e32 v63, 0x800, v63
	ds_read2_b64 v[64:67], v63 offset0:128 offset1:144
	v_pk_mul_f32 v[84:85], v[180:181], v[68:69] op_sel:[1,1] op_sel_hi:[0,1] neg_lo:[0,1]
	v_pk_fma_f32 v[84:85], v[180:181], v[68:69], v[84:85] op_sel_hi:[1,0,1]
	s_waitcnt lgkmcnt(0)
	v_pk_mul_f32 v[86:87], v[64:65], v[68:69] op_sel:[1,1] op_sel_hi:[0,1] neg_hi:[1,0]
	v_pk_fma_f32 v[86:87], v[64:65], v[68:69], v[86:87] op_sel_hi:[1,0,1]
	v_pk_mul_f32 v[64:65], v[66:67], v[84:85] op_sel:[1,1] op_sel_hi:[0,1] neg_hi:[1,0]
	v_pk_fma_f32 v[88:89], v[66:67], v[84:85], v[64:65] op_sel_hi:[1,0,1]
	v_xad_u32 v64, v50, 13, v10
	v_lshl_add_u32 v64, v64, 3, 0
	v_add_u32_e32 v64, 0x800, v64
	ds_read2_b64 v[66:69], v64 offset0:160 offset1:176
	v_pk_mul_f32 v[90:91], v[180:181], v[84:85] op_sel:[1,1] op_sel_hi:[0,1] neg_lo:[0,1]
	v_pk_fma_f32 v[84:85], v[180:181], v[84:85], v[90:91] op_sel_hi:[1,0,1]
	s_waitcnt lgkmcnt(0)
	v_pk_mul_f32 v[90:91], v[66:67], v[84:85] op_sel:[1,1] op_sel_hi:[0,1] neg_hi:[1,0]
	s_nop 0
	v_pk_fma_f32 v[90:91], v[66:67], v[84:85], v[90:91] op_sel_hi:[1,0,1]
	v_pk_mul_f32 v[66:67], v[180:181], v[84:85] op_sel:[1,1] op_sel_hi:[0,1] neg_lo:[0,1]
	v_pk_fma_f32 v[66:67], v[180:181], v[84:85], v[66:67] op_sel_hi:[1,0,1]
	s_nop 0
	v_pk_mul_f32 v[84:85], v[68:69], v[66:67] op_sel:[1,1] op_sel_hi:[0,1] neg_hi:[1,0]
	s_nop 0
	v_pk_fma_f32 v[84:85], v[68:69], v[66:67], v[84:85] op_sel_hi:[1,0,1]
	v_pk_mul_f32 v[68:69], v[180:181], v[66:67] op_sel:[1,1] op_sel_hi:[0,1] neg_lo:[0,1]
	v_pk_fma_f32 v[92:93], v[180:181], v[66:67], v[68:69] op_sel_hi:[1,0,1]
	v_xad_u32 v65, v50, 14, v10
	v_lshl_add_u32 v65, v65, 3, 0
	v_add_u32_e32 v65, 0x800, v65
	ds_read2_b64 v[66:69], v65 offset0:192 offset1:208
	v_pk_mul_f32 v[94:95], v[180:181], v[92:93] op_sel:[1,1] op_sel_hi:[0,1] neg_lo:[0,1]
	v_xad_u32 v10, v50, 15, v10
	s_waitcnt lgkmcnt(0)
	v_pk_mul_f32 v[96:97], v[66:67], v[92:93] op_sel:[1,1] op_sel_hi:[0,1] neg_hi:[1,0]
	v_lshl_add_u32 v10, v10, 3, 0
	v_pk_fma_f32 v[96:97], v[66:67], v[92:93], v[96:97] op_sel_hi:[1,0,1]
	v_pk_fma_f32 v[92:93], v[180:181], v[92:93], v[94:95] op_sel_hi:[1,0,1]
	s_nop 0
	v_pk_mul_f32 v[66:67], v[68:69], v[92:93] op_sel:[1,1] op_sel_hi:[0,1] neg_hi:[1,0]
	v_add_u32_e32 v101, 0x800, v10
	v_pk_fma_f32 v[94:95], v[68:69], v[92:93], v[66:67] op_sel_hi:[1,0,1]
	ds_read2_b64 v[66:69], v101 offset0:224 offset1:240
	v_pk_mul_f32 v[98:99], v[180:181], v[92:93] op_sel:[1,1] op_sel_hi:[0,1] neg_lo:[0,1]
	v_pk_fma_f32 v[92:93], v[180:181], v[92:93], v[98:99] op_sel_hi:[1,0,1]
	s_waitcnt lgkmcnt(0)
	v_pk_mul_f32 v[98:99], v[66:67], v[92:93] op_sel:[1,1] op_sel_hi:[0,1] neg_hi:[1,0]
	s_nop 0
	v_pk_fma_f32 v[66:67], v[66:67], v[92:93], v[98:99] op_sel_hi:[1,0,1]
	v_pk_mul_f32 v[98:99], v[180:181], v[92:93] op_sel:[1,1] op_sel_hi:[0,1] neg_lo:[0,1]
	v_pk_fma_f32 v[20:21], v[180:181], v[92:93], v[98:99] op_sel_hi:[1,0,1]
	s_nop 0
	v_pk_mul_f32 v[92:93], v[68:69], v[20:21] op_sel:[1,1] op_sel_hi:[0,1] neg_hi:[1,0]
	s_nop 0
	v_pk_fma_f32 v[68:69], v[68:69], v[20:21], v[92:93] op_sel_hi:[1,0,1]
	v_mov_b32_e32 v10, v1
	v_pk_add_f32 v[104:105], v[16:17], v[52:53]
	v_pk_add_f32 v[16:17], v[16:17], v[52:53] neg_lo:[0,1] neg_hi:[0,1]
	v_pk_add_f32 v[52:53], v[18:19], v[70:71]
	v_pk_add_f32 v[18:19], v[18:19], v[70:71] neg_lo:[0,1] neg_hi:[0,1]
	v_mov_b32_e32 v92, v164
	v_mov_b32_e32 v20, v165
	v_mov_b32_e32 v98, v166
	v_mov_b32_e32 v10, v167
	v_mov_b32_e32 v100, v168
	v_mov_b32_e32 v50, v169
	v_mov_b32_e32 v102, v170
	v_mov_b32_e32 v21, v171
	v_pk_mul_f32 v[70:71], v[102:103], v[18:19] op_sel:[0,1] op_sel_hi:[0,0] neg_lo:[0,1]
	v_pk_fma_f32 v[18:19], v[92:93], v[18:19], v[70:71] op_sel_hi:[0,1,1]
	v_pk_add_f32 v[70:71], v[22:23], v[72:73]
	v_pk_add_f32 v[22:23], v[22:23], v[72:73] neg_lo:[0,1] neg_hi:[0,1]
	s_nop 0
	v_pk_mul_f32 v[72:73], v[50:51], v[22:23] op_sel:[0,1] op_sel_hi:[0,0] neg_lo:[0,1]
	v_pk_fma_f32 v[22:23], v[20:21], v[22:23], v[72:73] op_sel_hi:[0,1,1]
	v_pk_add_f32 v[72:73], v[24:25], v[74:75]
	v_pk_add_f32 v[24:25], v[24:25], v[74:75] neg_lo:[0,1] neg_hi:[0,1]
	s_nop 0
	v_pk_mul_f32 v[74:75], v[100:101], v[24:25] op_sel:[0,1] op_sel_hi:[0,0] neg_lo:[0,1]
	v_pk_fma_f32 v[24:25], v[98:99], v[24:25], v[74:75] op_sel_hi:[0,1,1]
	v_pk_add_f32 v[74:75], v[28:29], v[76:77]
	v_pk_add_f32 v[28:29], v[28:29], v[76:77] neg_lo:[0,1] neg_hi:[0,1]
	s_nop 0
	v_pk_mul_f32 v[76:77], v[10:11], v[28:29] op_sel:[0,1] op_sel_hi:[0,0] neg_lo:[0,1]
	v_pk_fma_f32 v[28:29], v[10:11], v[28:29], v[76:77] op_sel_hi:[0,1,1]
	v_pk_add_f32 v[76:77], v[26:27], v[78:79]
	v_pk_add_f32 v[26:27], v[26:27], v[78:79] neg_lo:[0,1] neg_hi:[0,1]
	s_nop 0
	v_pk_mul_f32 v[78:79], v[98:99], v[26:27] op_sel:[0,1] op_sel_hi:[0,0] neg_lo:[0,1]
	v_pk_fma_f32 v[26:27], v[100:101], v[26:27], v[78:79] op_sel_hi:[0,1,1]
	v_pk_add_f32 v[78:79], v[30:31], v[80:81]
	v_pk_add_f32 v[30:31], v[30:31], v[80:81] neg_lo:[0,1] neg_hi:[0,1]
	s_nop 0
	v_pk_mul_f32 v[80:81], v[20:21], v[30:31] op_sel:[0,1] op_sel_hi:[0,0] neg_lo:[0,1]
	v_pk_fma_f32 v[30:31], v[50:51], v[30:31], v[80:81] op_sel_hi:[0,1,1]
	v_pk_add_f32 v[80:81], v[32:33], v[82:83]
	v_pk_add_f32 v[32:33], v[32:33], v[82:83] neg_lo:[0,1] neg_hi:[0,1]
	s_nop 0
	v_pk_mul_f32 v[82:83], v[92:93], v[32:33] op_sel:[0,1] op_sel_hi:[0,0] neg_lo:[0,1]
	v_pk_fma_f32 v[32:33], v[102:103], v[32:33], v[82:83] op_sel_hi:[0,1,1]
	v_pk_add_f32 v[82:83], v[34:35], v[86:87]
	v_pk_add_f32 v[34:35], v[34:35], v[86:87] neg_lo:[0,1] neg_hi:[0,1]
	s_nop 0
	v_xor_b32_e32 v86, 0x80000000, v35
	v_mov_b32_e32 v87, v34
	v_pk_add_f32 v[34:35], v[36:37], v[88:89]
	v_pk_add_f32 v[36:37], v[36:37], v[88:89] neg_lo:[0,1] neg_hi:[0,1]
	s_nop 0
	v_pk_mul_f32 v[88:89], v[92:93], v[36:37] op_sel:[0,1] op_sel_hi:[0,0] neg_lo:[0,1]
	v_pk_fma_f32 v[36:37], v[102:103], v[36:37], v[88:89] op_sel_hi:[0,1,1] neg_lo:[1,0,0] neg_hi:[1,0,0]
	v_pk_add_f32 v[88:89], v[38:39], v[90:91]
	v_pk_add_f32 v[38:39], v[38:39], v[90:91] neg_lo:[0,1] neg_hi:[0,1]
	s_nop 0
	v_pk_mul_f32 v[90:91], v[20:21], v[38:39] op_sel:[0,1] op_sel_hi:[0,0] neg_lo:[0,1]
	v_pk_fma_f32 v[38:39], v[50:51], v[38:39], v[90:91] op_sel_hi:[0,1,1] neg_lo:[1,0,0] neg_hi:[1,0,0]
	v_pk_add_f32 v[90:91], v[40:41], v[84:85]
	v_pk_add_f32 v[40:41], v[40:41], v[84:85] neg_lo:[0,1] neg_hi:[0,1]
	s_nop 0
	v_pk_mul_f32 v[84:85], v[98:99], v[40:41] op_sel:[0,1] op_sel_hi:[0,0] neg_lo:[0,1]
	v_pk_fma_f32 v[40:41], v[100:101], v[40:41], v[84:85] op_sel_hi:[0,1,1] neg_lo:[1,0,0] neg_hi:[1,0,0]
	v_pk_add_f32 v[84:85], v[44:45], v[96:97]
	v_pk_add_f32 v[44:45], v[44:45], v[96:97] neg_lo:[0,1] neg_hi:[0,1]
	s_nop 0
	v_pk_mul_f32 v[96:97], v[10:11], v[44:45] op_sel:[0,1] op_sel_hi:[0,0] neg_lo:[0,1]
	v_pk_fma_f32 v[44:45], v[10:11], v[44:45], v[96:97] op_sel_hi:[0,1,1] neg_lo:[1,0,0] neg_hi:[1,0,0]
	v_pk_add_f32 v[96:97], v[42:43], v[94:95]
	v_pk_add_f32 v[42:43], v[42:43], v[94:95] neg_lo:[0,1] neg_hi:[0,1]
	s_nop 0
	v_pk_mul_f32 v[94:95], v[100:101], v[42:43] op_sel:[0,1] op_sel_hi:[0,0] neg_lo:[0,1]
	v_pk_fma_f32 v[42:43], v[98:99], v[42:43], v[94:95] op_sel_hi:[0,1,1] neg_lo:[1,0,0] neg_hi:[1,0,0]
	v_pk_add_f32 v[94:95], v[46:47], v[66:67]
	v_pk_add_f32 v[46:47], v[46:47], v[66:67] neg_lo:[0,1] neg_hi:[0,1]
	s_nop 0
	v_pk_mul_f32 v[66:67], v[50:51], v[46:47] op_sel:[0,1] op_sel_hi:[0,0] neg_lo:[0,1]
	v_pk_fma_f32 v[46:47], v[20:21], v[46:47], v[66:67] op_sel_hi:[0,1,1] neg_lo:[1,0,0] neg_hi:[1,0,0]
	v_pk_add_f32 v[66:67], v[48:49], v[68:69]
	v_pk_add_f32 v[48:49], v[48:49], v[68:69] neg_lo:[0,1] neg_hi:[0,1]
	s_nop 0
	v_pk_mul_f32 v[68:69], v[102:103], v[48:49] op_sel:[0,1] op_sel_hi:[0,0] neg_lo:[0,1]
	v_pk_fma_f32 v[48:49], v[92:93], v[48:49], v[68:69] op_sel_hi:[0,1,1] neg_lo:[1,0,0] neg_hi:[1,0,0]
	v_pk_add_f32 v[92:93], v[52:53], v[34:35]
	v_pk_add_f32 v[34:35], v[52:53], v[34:35] neg_lo:[0,1] neg_hi:[0,1]
	v_pk_add_f32 v[68:69], v[104:105], v[82:83]
	v_pk_mul_f32 v[52:53], v[50:51], v[34:35] op_sel:[0,1] op_sel_hi:[0,0] neg_lo:[0,1]
	v_pk_fma_f32 v[34:35], v[20:21], v[34:35], v[52:53] op_sel_hi:[0,1,1]
	v_pk_add_f32 v[52:53], v[70:71], v[88:89]
	v_pk_add_f32 v[70:71], v[70:71], v[88:89] neg_lo:[0,1] neg_hi:[0,1]
	v_pk_add_f32 v[82:83], v[104:105], v[82:83] neg_lo:[0,1] neg_hi:[0,1]
	v_pk_mul_f32 v[88:89], v[10:11], v[70:71] op_sel:[0,1] op_sel_hi:[0,0] neg_lo:[0,1]
	v_pk_fma_f32 v[70:71], v[10:11], v[70:71], v[88:89] op_sel_hi:[0,1,1]
	v_pk_add_f32 v[88:89], v[72:73], v[90:91]
	v_pk_add_f32 v[72:73], v[72:73], v[90:91] neg_lo:[0,1] neg_hi:[0,1]
	s_nop 0
	v_pk_mul_f32 v[90:91], v[20:21], v[72:73] op_sel:[0,1] op_sel_hi:[0,0] neg_lo:[0,1]
	v_pk_fma_f32 v[72:73], v[50:51], v[72:73], v[90:91] op_sel_hi:[0,1,1]
	v_pk_add_f32 v[90:91], v[74:75], v[84:85]
	v_pk_add_f32 v[74:75], v[74:75], v[84:85] neg_lo:[0,1] neg_hi:[0,1]
	s_nop 0
	v_xor_b32_e32 v84, 0x80000000, v75
	v_mov_b32_e32 v85, v74
	v_pk_add_f32 v[74:75], v[76:77], v[96:97]
	v_pk_add_f32 v[76:77], v[76:77], v[96:97] neg_lo:[0,1] neg_hi:[0,1]
	s_nop 0
	v_pk_mul_f32 v[96:97], v[20:21], v[76:77] op_sel:[0,1] op_sel_hi:[0,0] neg_lo:[0,1]
	v_pk_fma_f32 v[76:77], v[50:51], v[76:77], v[96:97] op_sel_hi:[0,1,1] neg_lo:[1,0,0] neg_hi:[1,0,0]
	v_pk_add_f32 v[96:97], v[78:79], v[94:95]
	v_pk_add_f32 v[78:79], v[78:79], v[94:95] neg_lo:[0,1] neg_hi:[0,1]
	s_nop 0
	v_pk_mul_f32 v[94:95], v[10:11], v[78:79] op_sel:[0,1] op_sel_hi:[0,0] neg_lo:[0,1]
	v_pk_fma_f32 v[78:79], v[10:11], v[78:79], v[94:95] op_sel_hi:[0,1,1] neg_lo:[1,0,0] neg_hi:[1,0,0]
	v_pk_add_f32 v[94:95], v[80:81], v[66:67]
	v_pk_add_f32 v[66:67], v[80:81], v[66:67] neg_lo:[0,1] neg_hi:[0,1]
	s_nop 0
	v_pk_mul_f32 v[80:81], v[50:51], v[66:67] op_sel:[0,1] op_sel_hi:[0,0] neg_lo:[0,1]
	v_pk_fma_f32 v[66:67], v[20:21], v[66:67], v[80:81] op_sel_hi:[0,1,1] neg_lo:[1,0,0] neg_hi:[1,0,0]
	v_pk_add_f32 v[80:81], v[68:69], v[90:91]
	v_pk_add_f32 v[68:69], v[68:69], v[90:91] neg_lo:[0,1] neg_hi:[0,1]
	v_pk_add_f32 v[90:91], v[92:93], v[74:75]
	v_pk_add_f32 v[74:75], v[92:93], v[74:75] neg_lo:[0,1] neg_hi:[0,1]
	s_nop 0
	v_pk_mul_f32 v[92:93], v[10:11], v[74:75] op_sel:[0,1] op_sel_hi:[0,0] neg_lo:[0,1]
	v_pk_fma_f32 v[74:75], v[10:11], v[74:75], v[92:93] op_sel_hi:[0,1,1]
	v_pk_add_f32 v[92:93], v[52:53], v[96:97]
	v_pk_add_f32 v[52:53], v[52:53], v[96:97] neg_lo:[0,1] neg_hi:[0,1]
	s_nop 0
	v_xor_b32_e32 v96, 0x80000000, v53
	v_mov_b32_e32 v97, v52
	v_pk_add_f32 v[52:53], v[88:89], v[94:95]
	v_pk_add_f32 v[88:89], v[88:89], v[94:95] neg_lo:[0,1] neg_hi:[0,1]
	s_nop 0
	v_pk_mul_f32 v[94:95], v[10:11], v[88:89] op_sel:[0,1] op_sel_hi:[0,0] neg_lo:[0,1]
	v_pk_fma_f32 v[88:89], v[10:11], v[88:89], v[94:95] op_sel_hi:[0,1,1] neg_lo:[1,0,0] neg_hi:[1,0,0]
	v_pk_add_f32 v[94:95], v[80:81], v[92:93]
	v_pk_add_f32 v[80:81], v[80:81], v[92:93] neg_lo:[0,1] neg_hi:[0,1]
	v_pk_add_f32 v[92:93], v[90:91], v[52:53]
	v_pk_add_f32 v[52:53], v[90:91], v[52:53] neg_lo:[0,1] neg_hi:[0,1]
	s_nop 0
	v_xor_b32_e32 v90, 0x80000000, v53
	v_mov_b32_e32 v91, v52
	v_pk_add_f32 v[52:53], v[94:95], v[92:93]
	v_pk_add_f32 v[92:93], v[94:95], v[92:93] neg_lo:[0,1] neg_hi:[0,1]
	v_pk_add_f32 v[94:95], v[80:81], v[90:91]
	v_pk_add_f32 v[80:81], v[80:81], v[90:91] neg_lo:[0,1] neg_hi:[0,1]
	v_pk_add_f32 v[90:91], v[68:69], v[96:97]
	v_pk_add_f32 v[68:69], v[68:69], v[96:97] neg_lo:[0,1] neg_hi:[0,1]
	v_pk_add_f32 v[96:97], v[74:75], v[88:89]
	v_pk_add_f32 v[74:75], v[74:75], v[88:89] neg_lo:[0,1] neg_hi:[0,1]
	s_nop 0
	v_xor_b32_e32 v88, 0x80000000, v75
	v_mov_b32_e32 v89, v74
	v_pk_add_f32 v[74:75], v[90:91], v[96:97]
	v_pk_add_f32 v[90:91], v[90:91], v[96:97] neg_lo:[0,1] neg_hi:[0,1]
	v_pk_add_f32 v[96:97], v[68:69], v[88:89]
	v_pk_add_f32 v[68:69], v[68:69], v[88:89] neg_lo:[0,1] neg_hi:[0,1]
	v_pk_add_f32 v[88:89], v[82:83], v[84:85]
	v_pk_add_f32 v[82:83], v[82:83], v[84:85] neg_lo:[0,1] neg_hi:[0,1]
	v_pk_add_f32 v[84:85], v[34:35], v[76:77]
	v_pk_add_f32 v[34:35], v[34:35], v[76:77] neg_lo:[0,1] neg_hi:[0,1]
	s_nop 0
	v_pk_mul_f32 v[76:77], v[10:11], v[34:35] op_sel:[0,1] op_sel_hi:[0,0] neg_lo:[0,1]
	v_pk_fma_f32 v[34:35], v[10:11], v[34:35], v[76:77] op_sel_hi:[0,1,1]
	v_pk_add_f32 v[76:77], v[70:71], v[78:79]
	v_pk_add_f32 v[70:71], v[70:71], v[78:79] neg_lo:[0,1] neg_hi:[0,1]
	s_nop 0
	v_xor_b32_e32 v78, 0x80000000, v71
	v_mov_b32_e32 v79, v70
	v_pk_add_f32 v[70:71], v[72:73], v[66:67]
	v_pk_add_f32 v[66:67], v[72:73], v[66:67] neg_lo:[0,1] neg_hi:[0,1]
	s_nop 0
	v_pk_mul_f32 v[72:73], v[10:11], v[66:67] op_sel:[0,1] op_sel_hi:[0,0] neg_lo:[0,1]
	v_pk_fma_f32 v[66:67], v[10:11], v[66:67], v[72:73] op_sel_hi:[0,1,1] neg_lo:[1,0,0] neg_hi:[1,0,0]
	v_pk_add_f32 v[72:73], v[88:89], v[76:77]
	v_pk_add_f32 v[76:77], v[88:89], v[76:77] neg_lo:[0,1] neg_hi:[0,1]
	v_pk_add_f32 v[88:89], v[84:85], v[70:71]
	v_pk_add_f32 v[70:71], v[84:85], v[70:71] neg_lo:[0,1] neg_hi:[0,1]
	s_nop 0
	v_xor_b32_e32 v84, 0x80000000, v71
	v_mov_b32_e32 v85, v70
	v_pk_add_f32 v[70:71], v[72:73], v[88:89]
	v_pk_add_f32 v[72:73], v[72:73], v[88:89] neg_lo:[0,1] neg_hi:[0,1]
	v_pk_add_f32 v[88:89], v[76:77], v[84:85]
	v_pk_add_f32 v[76:77], v[76:77], v[84:85] neg_lo:[0,1] neg_hi:[0,1]
	v_pk_add_f32 v[84:85], v[82:83], v[78:79]
	v_pk_add_f32 v[78:79], v[82:83], v[78:79] neg_lo:[0,1] neg_hi:[0,1]
	v_pk_add_f32 v[82:83], v[34:35], v[66:67]
	v_pk_add_f32 v[34:35], v[34:35], v[66:67] neg_lo:[0,1] neg_hi:[0,1]
	s_nop 0
	v_xor_b32_e32 v66, 0x80000000, v35
	v_mov_b32_e32 v67, v34
	v_pk_add_f32 v[34:35], v[84:85], v[82:83]
	v_pk_add_f32 v[82:83], v[84:85], v[82:83] neg_lo:[0,1] neg_hi:[0,1]
	v_pk_add_f32 v[84:85], v[78:79], v[66:67]
	v_pk_add_f32 v[66:67], v[78:79], v[66:67] neg_lo:[0,1] neg_hi:[0,1]
	v_pk_add_f32 v[78:79], v[16:17], v[86:87]
	v_pk_add_f32 v[16:17], v[16:17], v[86:87] neg_lo:[0,1] neg_hi:[0,1]
	v_pk_add_f32 v[86:87], v[18:19], v[36:37]
	v_pk_add_f32 v[18:19], v[18:19], v[36:37] neg_lo:[0,1] neg_hi:[0,1]
	s_nop 0
	v_pk_mul_f32 v[36:37], v[50:51], v[18:19] op_sel:[0,1] op_sel_hi:[0,0] neg_lo:[0,1]
	v_pk_fma_f32 v[18:19], v[20:21], v[18:19], v[36:37] op_sel_hi:[0,1,1]
	v_pk_add_f32 v[36:37], v[22:23], v[38:39]
	v_pk_add_f32 v[22:23], v[22:23], v[38:39] neg_lo:[0,1] neg_hi:[0,1]
	s_nop 0
	v_pk_mul_f32 v[38:39], v[10:11], v[22:23] op_sel:[0,1] op_sel_hi:[0,0] neg_lo:[0,1]
	v_pk_fma_f32 v[22:23], v[10:11], v[22:23], v[38:39] op_sel_hi:[0,1,1]
	v_pk_add_f32 v[38:39], v[24:25], v[40:41]
	v_pk_add_f32 v[24:25], v[24:25], v[40:41] neg_lo:[0,1] neg_hi:[0,1]
	s_nop 0
	v_pk_mul_f32 v[40:41], v[20:21], v[24:25] op_sel:[0,1] op_sel_hi:[0,0] neg_lo:[0,1]
	v_pk_fma_f32 v[24:25], v[50:51], v[24:25], v[40:41] op_sel_hi:[0,1,1]
	v_pk_add_f32 v[40:41], v[28:29], v[44:45]
	v_pk_add_f32 v[28:29], v[28:29], v[44:45] neg_lo:[0,1] neg_hi:[0,1]
	s_nop 0
	v_xor_b32_e32 v44, 0x80000000, v29
	v_mov_b32_e32 v45, v28
	v_pk_add_f32 v[28:29], v[26:27], v[42:43]
	v_pk_add_f32 v[26:27], v[26:27], v[42:43] neg_lo:[0,1] neg_hi:[0,1]
	s_nop 0
	v_pk_mul_f32 v[42:43], v[20:21], v[26:27] op_sel:[0,1] op_sel_hi:[0,0] neg_lo:[0,1]
	v_pk_fma_f32 v[26:27], v[50:51], v[26:27], v[42:43] op_sel_hi:[0,1,1] neg_lo:[1,0,0] neg_hi:[1,0,0]
	v_pk_add_f32 v[42:43], v[30:31], v[46:47]
	v_pk_add_f32 v[30:31], v[30:31], v[46:47] neg_lo:[0,1] neg_hi:[0,1]
	s_nop 0
	v_pk_mul_f32 v[46:47], v[10:11], v[30:31] op_sel:[0,1] op_sel_hi:[0,0] neg_lo:[0,1]
	v_pk_fma_f32 v[30:31], v[10:11], v[30:31], v[46:47] op_sel_hi:[0,1,1] neg_lo:[1,0,0] neg_hi:[1,0,0]
	v_pk_add_f32 v[46:47], v[32:33], v[48:49]
	v_pk_add_f32 v[32:33], v[32:33], v[48:49] neg_lo:[0,1] neg_hi:[0,1]
	s_nop 0
	v_pk_mul_f32 v[48:49], v[50:51], v[32:33] op_sel:[0,1] op_sel_hi:[0,0] neg_lo:[0,1]
	v_pk_fma_f32 v[20:21], v[20:21], v[32:33], v[48:49] op_sel_hi:[0,1,1] neg_lo:[1,0,0] neg_hi:[1,0,0]
	v_pk_add_f32 v[48:49], v[86:87], v[28:29]
	v_pk_add_f32 v[28:29], v[86:87], v[28:29] neg_lo:[0,1] neg_hi:[0,1]
	v_pk_add_f32 v[32:33], v[78:79], v[40:41]
	v_pk_add_f32 v[40:41], v[78:79], v[40:41] neg_lo:[0,1] neg_hi:[0,1]
	v_pk_mul_f32 v[78:79], v[10:11], v[28:29] op_sel:[0,1] op_sel_hi:[0,0] neg_lo:[0,1]
	v_pk_fma_f32 v[28:29], v[10:11], v[28:29], v[78:79] op_sel_hi:[0,1,1]
	v_pk_add_f32 v[78:79], v[36:37], v[42:43]
	v_pk_add_f32 v[36:37], v[36:37], v[42:43] neg_lo:[0,1] neg_hi:[0,1]
	s_nop 0
	v_xor_b32_e32 v42, 0x80000000, v37
	v_mov_b32_e32 v43, v36
	v_pk_add_f32 v[36:37], v[38:39], v[46:47]
	v_pk_add_f32 v[38:39], v[38:39], v[46:47] neg_lo:[0,1] neg_hi:[0,1]
	s_nop 0
	v_pk_mul_f32 v[46:47], v[10:11], v[38:39] op_sel:[0,1] op_sel_hi:[0,0] neg_lo:[0,1]
	v_pk_fma_f32 v[38:39], v[10:11], v[38:39], v[46:47] op_sel_hi:[0,1,1] neg_lo:[1,0,0] neg_hi:[1,0,0]
	v_pk_add_f32 v[46:47], v[32:33], v[78:79]
	v_pk_add_f32 v[32:33], v[32:33], v[78:79] neg_lo:[0,1] neg_hi:[0,1]
	v_pk_add_f32 v[78:79], v[48:49], v[36:37]
	v_pk_add_f32 v[36:37], v[48:49], v[36:37] neg_lo:[0,1] neg_hi:[0,1]
	s_nop 0
	v_pk_add_f32 v[86:87], v[32:33], v[36:37] op_sel:[0,1] op_sel_hi:[1,0] neg_lo:[0,1]
	v_pk_add_f32 v[32:33], v[32:33], v[36:37] op_sel:[0,1] op_sel_hi:[1,0] neg_hi:[0,1]
	v_pk_add_f32 v[48:49], v[40:41], v[42:43]
	v_pk_add_f32 v[40:41], v[40:41], v[42:43] neg_lo:[0,1] neg_hi:[0,1]
	v_pk_add_f32 v[42:43], v[28:29], v[38:39]
	v_pk_add_f32 v[28:29], v[28:29], v[38:39] neg_lo:[0,1] neg_hi:[0,1]
	v_pk_add_f32 v[36:37], v[46:47], v[78:79] neg_lo:[0,1] neg_hi:[0,1]
	v_xor_b32_e32 v38, 0x80000000, v29
	v_mov_b32_e32 v39, v28
	v_pk_add_f32 v[28:29], v[48:49], v[42:43]
	v_pk_add_f32 v[42:43], v[48:49], v[42:43] neg_lo:[0,1] neg_hi:[0,1]
	v_pk_add_f32 v[48:49], v[40:41], v[38:39]
	v_pk_add_f32 v[38:39], v[40:41], v[38:39] neg_lo:[0,1] neg_hi:[0,1]
	v_pk_add_f32 v[40:41], v[16:17], v[44:45]
	v_pk_add_f32 v[16:17], v[16:17], v[44:45] neg_lo:[0,1] neg_hi:[0,1]
	v_pk_add_f32 v[44:45], v[18:19], v[26:27]
	v_pk_add_f32 v[18:19], v[18:19], v[26:27] neg_lo:[0,1] neg_hi:[0,1]
	s_nop 0
	v_pk_mul_f32 v[26:27], v[10:11], v[18:19] op_sel:[0,1] op_sel_hi:[0,0] neg_lo:[0,1]
	v_pk_fma_f32 v[18:19], v[10:11], v[18:19], v[26:27] op_sel_hi:[0,1,1]
	v_pk_add_f32 v[26:27], v[22:23], v[30:31]
	v_pk_add_f32 v[22:23], v[22:23], v[30:31] neg_lo:[0,1] neg_hi:[0,1]
	s_nop 0
	v_xor_b32_e32 v30, 0x80000000, v23
	v_mov_b32_e32 v31, v22
	v_pk_add_f32 v[22:23], v[24:25], v[20:21]
	v_pk_add_f32 v[20:21], v[24:25], v[20:21] neg_lo:[0,1] neg_hi:[0,1]
	s_nop 0
	v_pk_mul_f32 v[24:25], v[10:11], v[20:21] op_sel:[0,1] op_sel_hi:[0,0] neg_lo:[0,1]
	v_pk_fma_f32 v[20:21], v[10:11], v[20:21], v[24:25] op_sel_hi:[0,1,1] neg_lo:[1,0,0] neg_hi:[1,0,0]
	v_pk_add_f32 v[24:25], v[40:41], v[26:27]
	v_pk_add_f32 v[26:27], v[40:41], v[26:27] neg_lo:[0,1] neg_hi:[0,1]
	v_pk_add_f32 v[40:41], v[44:45], v[22:23]
	v_pk_add_f32 v[22:23], v[44:45], v[22:23] neg_lo:[0,1] neg_hi:[0,1]
	s_nop 0
	v_xor_b32_e32 v44, 0x80000000, v23
	v_mov_b32_e32 v45, v22
	v_pk_add_f32 v[22:23], v[24:25], v[40:41]
	v_pk_add_f32 v[24:25], v[24:25], v[40:41] neg_lo:[0,1] neg_hi:[0,1]
	v_pk_add_f32 v[40:41], v[26:27], v[44:45]
	v_pk_add_f32 v[26:27], v[26:27], v[44:45] neg_lo:[0,1] neg_hi:[0,1]
	v_pk_add_f32 v[44:45], v[16:17], v[30:31]
	v_pk_add_f32 v[16:17], v[16:17], v[30:31] neg_lo:[0,1] neg_hi:[0,1]
	v_pk_add_f32 v[30:31], v[18:19], v[20:21]
	v_pk_add_f32 v[18:19], v[18:19], v[20:21] neg_lo:[0,1] neg_hi:[0,1]
	s_nop 0
	v_xor_b32_e32 v20, 0x80000000, v19
	v_mov_b32_e32 v21, v18
	v_pk_add_f32 v[18:19], v[44:45], v[30:31]
	v_pk_add_f32 v[30:31], v[44:45], v[30:31] neg_lo:[0,1] neg_hi:[0,1]
	v_pk_add_f32 v[44:45], v[16:17], v[20:21]
	v_pk_add_f32 v[16:17], v[16:17], v[20:21] neg_lo:[0,1] neg_hi:[0,1]
	v_pk_add_f32 v[20:21], v[46:47], v[78:79]
	ds_write2_b64 v13, v[52:53], v[20:21] offset1:16
	ds_write2_b64 v15, v[70:71], v[22:23] offset0:32 offset1:48
	ds_write2_b64 v51, v[74:75], v[28:29] offset0:64 offset1:80
	ds_write2_b64 v54, v[34:35], v[18:19] offset0:96 offset1:112
	ds_write2_b64 v55, v[94:95], v[86:87] offset0:128 offset1:144
	ds_write2_b64 v56, v[88:89], v[40:41] offset0:160 offset1:176
	ds_write2_b64 v57, v[96:97], v[48:49] offset0:192 offset1:208
	ds_write2_b64 v58, v[84:85], v[44:45] offset0:224 offset1:240
	ds_write2_b64 v59, v[92:93], v[36:37] offset1:16
	ds_write2_b64 v60, v[72:73], v[24:25] offset0:32 offset1:48
	ds_write2_b64 v61, v[90:91], v[42:43] offset0:64 offset1:80
	ds_write2_b64 v62, v[82:83], v[30:31] offset0:96 offset1:112
	ds_write2_b64 v63, v[80:81], v[32:33] offset0:128 offset1:144
	ds_write2_b64 v64, v[76:77], v[26:27] offset0:160 offset1:176
	ds_write2_b64 v65, v[68:69], v[38:39] offset0:192 offset1:208
	ds_write2_b64 v101, v[66:67], v[16:17] offset0:224 offset1:240
	v_mov_b32_e32 v10, v173
	s_waitcnt lgkmcnt(0)
	s_barrier
	v_mov_b32_e32 v58, v178
	v_mov_b32_e32 v59, v179
	v_lshl_add_u32 v10, v10, 3, 0
	ds_read_b64 v[34:35], v10
	ds_read_b64 v[36:37], v10 offset:4224
	ds_read_b64 v[38:39], v10 offset:8448
	ds_read_b64 v[40:41], v10 offset:12672
	ds_read_b64 v[42:43], v10 offset:16896
	ds_read_b64 v[44:45], v10 offset:21120
	ds_read_b64 v[50:51], v10 offset:25344
	ds_read_b64 v[52:53], v10 offset:29568
	ds_read_b64 v[54:55], v10 offset:33792
	ds_read_b64 v[56:57], v10 offset:38016
	ds_read_b64 v[64:65], v10 offset:42240
	ds_read_b64 v[74:75], v10 offset:46464
	ds_read_b64 v[76:77], v10 offset:50688
	ds_read_b64 v[78:79], v10 offset:54912
	ds_read_b64 v[80:81], v10 offset:59136
	ds_read_b64 v[82:83], v10 offset:63360
	v_add_u32_e32 v13, 0x10800, v10
	v_add_u32_e32 v15, 0x11880, v10
	v_add_u32_e32 v16, 0x12900, v10
	v_add_u32_e32 v17, 0x13980, v10
	ds_read_b64 v[84:85], v13
	ds_read_b64 v[86:87], v15
	ds_read_b64 v[88:89], v16
	ds_read_b64 v[92:93], v17
	v_add_u32_e32 v13, 0x14a00, v10
	v_add_u32_e32 v15, 0x15a80, v10
	v_add_u32_e32 v16, 0x16b00, v10
	v_add_u32_e32 v17, 0x17b80, v10
	ds_read_b64 v[96:97], v13
	ds_read_b64 v[98:99], v15
	ds_read_b64 v[94:95], v16
	ds_read_b64 v[90:91], v17
	v_add_u32_e32 v13, 0x18c00, v10
	v_add_u32_e32 v15, 0x19c80, v10
	v_add_u32_e32 v16, 0x1ad00, v10
	v_add_u32_e32 v17, 0x1bd80, v10
	ds_read_b64 v[72:73], v13
	ds_read_b64 v[70:71], v15
	ds_read_b64 v[68:69], v16
	ds_read_b64 v[66:67], v17
	v_add_u32_e32 v13, 0x1ce00, v10
	v_add_u32_e32 v15, 0x1de80, v10
	v_add_u32_e32 v16, 0x1ef00, v10
	v_add_u32_e32 v10, 0x1ff80, v10
	ds_read_b64 v[62:63], v13
	ds_read_b64 v[60:61], v15
	ds_read_b64 v[100:101], v16
	ds_read_b64 v[102:103], v10
	s_mov_b32 s43, s95
	v_mov_b32_e32 v10, v1
	s_lshl_b64 s[0:1], s[42:43], 2
	v_readlane_b32 s2, v251, 46
	s_add_u32 s0, s2, s0
	v_readlane_b32 s2, v251, 48
	v_readlane_b32 s6, v251, 52
	v_mov_b32_e32 v24, v164
	v_mov_b32_e32 v32, v165
	v_mov_b32_e32 v28, v166
	v_mov_b32_e32 v46, v167
	v_mov_b32_e32 v48, v168
	v_mov_b32_e32 v30, v169
	v_mov_b32_e32 v26, v170
	v_mov_b32_e32 v10, v171
	v_mov_b32_e32 v16, v183
	v_mov_b32_e32 v19, v184
	s_addc_u32 s1, s2, s1
	v_readlane_b32 s7, v251, 53
	s_waitcnt lgkmcnt(0)
	s_barrier
	global_load_dword v13, v11, s[0:1]
	s_and_b64 s[0:1], s[6:7], exec
	s_movk_i32 s0, 0x800
	s_cselect_b32 s2, 0x400, s0
	v_readlane_b32 s24, v251, 50
	s_add_i32 s4, s2, s24
	s_mul_i32 s0, s4, 0x8200
	v_readlane_b32 s3, v251, 18
	s_mul_hi_i32 s1, s4, 0x8200
	s_add_u32 s0, s3, s0
	v_readlane_b32 s3, v251, 20
	s_addc_u32 s1, s3, s1
	s_lshl_b32 s2, s2, 2
	v_mov_b32_e32 v10, s2
	v_readlane_b32 s2, v251, 42
	v_readlane_b32 s3, v251, 43
	v_readlane_b32 s8, v250, 23
	v_readlane_b32 s9, v250, 24
	v_ashrrev_i32_e32 v15, 31, v14
	v_lshl_add_u64 v[22:23], v[14:15], 2, s[70:71]
	v_readlane_b32 s22, v250, 37
	global_load_dword v197, v10, s[2:3]
	s_add_i32 s2, s4, 0xc00
	s_ashr_i32 s3, s2, 31
	s_lshl_b64 s[2:3], s[2:3], 2
	s_add_u32 s2, s8, s2
	s_addc_u32 s3, s9, s3
	global_load_dword v198, v11, s[2:3]
	s_add_i32 s2, s4, 0x1800
	s_ashr_i32 s3, s2, 31
	s_lshl_b64 s[2:3], s[2:3], 2
	s_add_u32 s2, s8, s2
	s_addc_u32 s3, s9, s3
	global_load_dword v199, v11, s[2:3]
	v_readlane_b32 s2, v251, 40
	v_readlane_b32 s3, v251, 41
	v_cmp_lt_i32_e32 vcc, 0, v14
	v_mov_b32_e32 v17, 0
	v_lshl_add_u64 v[20:21], v[14:15], 1, s[0:1]
	v_mov_b32_e32 v18, 0
	v_readlane_b32 s25, v251, 51
	global_load_dword v200, v10, s[2:3]
	v_readlane_b32 s10, v250, 25
	v_lshlrev_b32_e32 v241, 1, v14
	v_lshlrev_b32_e32 v242, 2, v14
	v_add_u32_e32 v242, 0x1000, v242
	global_load_dword v190, v242, s[70:71] offset:-4096
	global_load_ushort v202, v241, s[0:1] offset:-2
	global_load_ushort v203, v241, s[0:1]
	global_load_ushort v204, v241, s[0:1] offset:2
	global_load_dword v205, v242, s[64:65] offset:-4096
	global_load_dword v206, v242, s[70:71] offset:-2048
	global_load_ushort v207, v241, s[0:1] offset:1022
	global_load_ushort v208, v241, s[0:1] offset:1024
	global_load_ushort v209, v241, s[0:1] offset:1026
	global_load_dword v210, v242, s[64:65] offset:-2048
	global_load_dword v211, v242, s[70:71]
	global_load_ushort v212, v241, s[0:1] offset:2046
	global_load_ushort v213, v241, s[0:1] offset:2048
	global_load_ushort v214, v241, s[0:1] offset:2050
	global_load_dword v215, v242, s[64:65]
	global_load_dword v216, v242, s[70:71] offset:2048
	global_load_ushort v217, v241, s[0:1] offset:3070
	global_load_ushort v218, v241, s[0:1] offset:3072
	global_load_ushort v219, v241, s[0:1] offset:3074
	global_load_dword v220, v242, s[64:65] offset:2048
	v_lshlrev_b32_e32 v241, 1, v14
	v_add_u32_e32 v241, 0x1000, v241
	v_lshlrev_b32_e32 v242, 2, v14
	v_add_u32_e32 v242, 0x3000, v242
	global_load_dword v221, v242, s[70:71] offset:-4096
	global_load_ushort v222, v241, s[0:1] offset:-2
	global_load_ushort v223, v241, s[0:1]
	global_load_ushort v224, v241, s[0:1] offset:2
	global_load_dword v225, v242, s[64:65] offset:-4096
	global_load_dword v226, v242, s[70:71] offset:-2048
	global_load_ushort v227, v241, s[0:1] offset:1022
	global_load_ushort v228, v241, s[0:1] offset:1024
	global_load_ushort v229, v241, s[0:1] offset:1026
	global_load_dword v230, v242, s[64:65] offset:-2048
	global_load_dword v231, v242, s[70:71]
	global_load_ushort v232, v241, s[0:1] offset:2046
	global_load_ushort v233, v241, s[0:1] offset:2048
	global_load_ushort v234, v241, s[0:1] offset:2050
	global_load_dword v235, v242, s[64:65]
	global_load_dword v236, v242, s[70:71] offset:2048
	global_load_ushort v237, v241, s[0:1] offset:3070
	global_load_ushort v238, v241, s[0:1] offset:3072
	global_load_ushort v239, v241, s[0:1] offset:3074
	global_load_dword v240, v242, s[64:65] offset:2048
	s_waitcnt vmcnt(20)
	v_mov_b32_e32 v10, v190
	v_readlane_b32 s11, v250, 26
	v_readlane_b32 s12, v250, 27
	v_readlane_b32 s13, v250, 28
	v_readlane_b32 s14, v250, 29
	v_readlane_b32 s15, v250, 30
	v_readlane_b32 s16, v250, 31
	v_readlane_b32 s17, v250, 32
	v_readlane_b32 s18, v250, 33
	v_readlane_b32 s19, v250, 34
	v_readlane_b32 s20, v250, 35
	v_readlane_b32 s21, v250, 36
	v_readlane_b32 s23, v250, 38
	s_and_saveexec_b64 s[2:3], vcc
	s_movk_i32 s22, 0x3fff
	s_cbranch_execz .LBB0_636
	v_mov_b32_e32 v18, v202
	s_nop 0
	v_lshlrev_b32_e32 v18, 16, v18

.LBB0_638:
	s_or_b64 exec, exec, s[2:3]
	v_add_f32_e32 v6, 0, v6
	v_add_f32_e32 v6, v6, v7
	v_add_f32_e32 v6, v6, v8
	v_add_f32_e32 v6, v6, v9
	v_add_f32_e32 v2, v6, v2
	v_add_f32_e32 v2, v2, v3
	v_add_f32_e32 v2, v2, v4
	v_add_f32_e32 v27, v2, v5
	v_pk_fma_f32 v[2:3], v[58:59], s[90:91], v[58:59] op_sel:[1,0,0] op_sel_hi:[0,1,1]
	v_pk_mul_f32 v[4:5], v[58:59], v[2:3] op_sel:[1,1] op_sel_hi:[0,1] neg_lo:[0,1]
	v_pk_fma_f32 v[4:5], v[58:59], v[2:3], v[4:5] op_sel_hi:[1,0,1]
	s_xor_b64 s[2:3], s[6:7], -1
	v_pk_mul_f32 v[6:7], v[58:59], v[4:5] op_sel:[1,1] op_sel_hi:[0,1] neg_lo:[0,1]
	v_pk_fma_f32 v[6:7], v[58:59], v[4:5], v[6:7] op_sel_hi:[1,0,1]
	s_brev_b32 s6, 28
	v_pk_mul_f32 v[8:9], v[58:59], v[6:7] op_sel:[1,1] op_sel_hi:[0,1] neg_lo:[0,1]
	v_pk_fma_f32 v[104:105], v[58:59], v[6:7], v[8:9] op_sel_hi:[1,0,1]
	v_div_scale_f32 v29, s[4:5], v27, v27, s6
	v_pk_mul_f32 v[8:9], v[58:59], v[104:105] op_sel:[1,1] op_sel_hi:[0,1] neg_lo:[0,1]
	v_pk_fma_f32 v[106:107], v[58:59], v[104:105], v[8:9] op_sel_hi:[1,0,1]
	s_mov_b32 s4, s45
	v_pk_mul_f32 v[8:9], v[58:59], v[106:107] op_sel:[1,1] op_sel_hi:[0,1] neg_lo:[0,1]
	v_pk_fma_f32 v[108:109], v[58:59], v[106:107], v[8:9] op_sel_hi:[1,0,1]
	s_mov_b32 s5, s94
	v_pk_mul_f32 v[8:9], v[58:59], v[108:109] op_sel:[1,1] op_sel_hi:[0,1] neg_lo:[0,1]
	v_pk_fma_f32 v[110:111], v[58:59], v[108:109], v[8:9] op_sel_hi:[1,0,1]
	s_mov_b32 s44, s94
	v_pk_mul_f32 v[8:9], v[58:59], v[110:111] op_sel:[1,1] op_sel_hi:[0,1] neg_lo:[0,1]
	v_pk_fma_f32 v[112:113], v[58:59], v[110:111], v[8:9] op_sel_hi:[1,0,1]
	v_rcp_f32_e32 v31, v29
	v_pk_mul_f32 v[8:9], v[58:59], v[112:113] op_sel:[1,1] op_sel_hi:[0,1] neg_lo:[0,1]
	v_pk_fma_f32 v[114:115], v[58:59], v[112:113], v[8:9] op_sel_hi:[1,0,1]
	v_fma_f32 v33, -v29, v31, 1.0
	v_pk_mul_f32 v[8:9], v[58:59], v[114:115] op_sel:[1,1] op_sel_hi:[0,1] neg_lo:[0,1]
	v_pk_fma_f32 v[118:119], v[58:59], v[114:115], v[8:9] op_sel_hi:[1,0,1]
	v_fmac_f32_e32 v31, v33, v31
	v_pk_mul_f32 v[8:9], v[58:59], v[118:119] op_sel:[1,1] op_sel_hi:[0,1] neg_lo:[0,1]
	v_pk_fma_f32 v[122:123], v[58:59], v[118:119], v[8:9] op_sel_hi:[1,0,1]
	v_div_scale_f32 v33, vcc, s6, v27, s6
	v_pk_mul_f32 v[8:9], v[58:59], v[122:123] op_sel:[1,1] op_sel_hi:[0,1] neg_lo:[0,1]
	v_pk_fma_f32 v[120:121], v[58:59], v[122:123], v[8:9] op_sel_hi:[1,0,1]
	v_mul_f32_e32 v47, v33, v31
	v_pk_mul_f32 v[8:9], v[58:59], v[120:121] op_sel:[1,1] op_sel_hi:[0,1] neg_lo:[0,1]
	v_pk_fma_f32 v[116:117], v[58:59], v[120:121], v[8:9] op_sel_hi:[1,0,1]
	v_fma_f32 v49, -v29, v47, v33
	v_pk_mul_f32 v[8:9], v[58:59], v[116:117] op_sel:[1,1] op_sel_hi:[0,1] neg_lo:[0,1]
	v_pk_fma_f32 v[124:125], v[58:59], v[116:117], v[8:9] op_sel_hi:[1,0,1]
	v_fmac_f32_e32 v47, v49, v31
	v_pk_mul_f32 v[8:9], v[58:59], v[124:125] op_sel:[1,1] op_sel_hi:[0,1] neg_lo:[0,1]
	v_pk_fma_f32 v[126:127], v[58:59], v[124:125], v[8:9] op_sel_hi:[1,0,1]
	v_fma_f32 v29, -v29, v47, v33
	v_pk_mul_f32 v[8:9], v[58:59], v[126:127] op_sel:[1,1] op_sel_hi:[0,1] neg_lo:[0,1]
	v_pk_fma_f32 v[128:129], v[58:59], v[126:127], v[8:9] op_sel_hi:[1,0,1]
	v_div_fmas_f32 v29, v29, v31, v47
	v_pk_mul_f32 v[8:9], v[58:59], v[128:129] op_sel:[1,1] op_sel_hi:[0,1] neg_lo:[0,1]
	v_pk_fma_f32 v[130:131], v[58:59], v[128:129], v[8:9] op_sel_hi:[1,0,1]
	v_div_fixup_f32 v201, v29, v27, s6
	v_pk_mul_f32 v[8:9], v[58:59], v[130:131] op_sel:[1,1] op_sel_hi:[0,1] neg_lo:[0,1]
	v_pk_fma_f32 v[132:133], v[58:59], v[130:131], v[8:9] op_sel_hi:[1,0,1]
	s_mov_b32 s8, 0x3f74fa0b
	v_pk_mul_f32 v[8:9], v[58:59], v[132:133] op_sel:[1,1] op_sel_hi:[0,1] neg_lo:[0,1]
	v_pk_fma_f32 v[134:135], v[58:59], v[132:133], v[8:9] op_sel_hi:[1,0,1]
	s_mov_b32 s10, 0x3f54db31
	v_pk_mul_f32 v[8:9], v[58:59], v[134:135] op_sel:[1,1] op_sel_hi:[0,1] neg_lo:[0,1]
	v_pk_fma_f32 v[136:137], v[58:59], v[134:135], v[8:9] op_sel_hi:[1,0,1]
	s_mov_b32 s14, 0x3f226799
	v_pk_mul_f32 v[8:9], v[58:59], v[136:137] op_sel:[1,1] op_sel_hi:[0,1] neg_lo:[0,1]
	v_pk_fma_f32 v[138:139], v[58:59], v[136:137], v[8:9] op_sel_hi:[1,0,1]
	s_mov_b32 s16, 0x3ef15aea
	v_pk_mul_f32 v[8:9], v[58:59], v[138:139] op_sel:[1,1] op_sel_hi:[0,1] neg_lo:[0,1]
	v_pk_fma_f32 v[140:141], v[58:59], v[138:139], v[8:9] op_sel_hi:[1,0,1]
	s_mov_b32 s18, 0x3e94a031
	v_pk_mul_f32 v[8:9], v[58:59], v[140:141] op_sel:[1,1] op_sel_hi:[0,1] neg_lo:[0,1]
	v_pk_fma_f32 v[142:143], v[58:59], v[140:141], v[8:9] op_sel_hi:[1,0,1]
	s_and_b64 vcc, exec, s[2:3]
	v_pk_mul_f32 v[8:9], v[58:59], v[142:143] op_sel:[1,1] op_sel_hi:[0,1] neg_lo:[0,1]
	v_pk_fma_f32 v[144:145], v[58:59], v[142:143], v[8:9] op_sel_hi:[1,0,1]
	s_movk_i32 s43, 0x4000
	v_pk_mul_f32 v[8:9], v[58:59], v[144:145] op_sel:[1,1] op_sel_hi:[0,1] neg_lo:[0,1]
	v_pk_fma_f32 v[146:147], v[58:59], v[144:145], v[8:9] op_sel_hi:[1,0,1]
	s_movk_i32 s48, 0xfc00
	v_pk_mul_f32 v[8:9], v[58:59], v[146:147] op_sel:[1,1] op_sel_hi:[0,1] neg_lo:[0,1]
	v_pk_fma_f32 v[148:149], v[58:59], v[146:147], v[8:9] op_sel_hi:[1,0,1]
	s_movk_i32 s49, 0xfa00
	v_pk_mul_f32 v[8:9], v[58:59], v[148:149] op_sel:[1,1] op_sel_hi:[0,1] neg_lo:[0,1]
	v_pk_fma_f32 v[150:151], v[58:59], v[148:149], v[8:9] op_sel_hi:[1,0,1]
	s_movk_i32 s50, 0xf800
	v_pk_mul_f32 v[8:9], v[58:59], v[150:151] op_sel:[1,1] op_sel_hi:[0,1] neg_lo:[0,1]
	v_pk_fma_f32 v[152:153], v[58:59], v[150:151], v[8:9] op_sel_hi:[1,0,1]
	s_movk_i32 s51, 0xf600
	v_pk_mul_f32 v[8:9], v[58:59], v[152:153] op_sel:[1,1] op_sel_hi:[0,1] neg_lo:[0,1]
	v_pk_fma_f32 v[154:155], v[58:59], v[152:153], v[8:9] op_sel_hi:[1,0,1]
	s_movk_i32 s57, 0xf400
	v_pk_mul_f32 v[8:9], v[58:59], v[154:155] op_sel:[1,1] op_sel_hi:[0,1] neg_lo:[0,1]
	v_pk_fma_f32 v[156:157], v[58:59], v[154:155], v[8:9] op_sel_hi:[1,0,1]
	s_movk_i32 s58, 0xf200
	v_pk_mul_f32 v[8:9], v[58:59], v[156:157] op_sel:[1,1] op_sel_hi:[0,1] neg_lo:[0,1]
	v_pk_fma_f32 v[8:9], v[58:59], v[156:157], v[8:9] op_sel_hi:[1,0,1]
	s_nop 0
	v_pk_mul_f32 v[58:59], v[102:103], v[8:9] op_sel:[1,1] op_sel_hi:[0,1] neg_hi:[1,0]
	s_movk_i32 s59, 0xf000
	v_pk_fma_f32 v[8:9], v[102:103], v[8:9], v[58:59] op_sel_hi:[1,0,1]
	v_pk_mul_f32 v[58:59], v[100:101], v[156:157] op_sel:[1,1] op_sel_hi:[0,1] neg_hi:[1,0]
	s_movk_i32 s60, 0xee00
	v_pk_fma_f32 v[58:59], v[100:101], v[156:157], v[58:59] op_sel_hi:[1,0,1]
	v_pk_mul_f32 v[100:101], v[60:61], v[154:155] op_sel:[1,1] op_sel_hi:[0,1] neg_hi:[1,0]
	s_movk_i32 s61, 0xec00
	v_pk_fma_f32 v[60:61], v[60:61], v[154:155], v[100:101] op_sel_hi:[1,0,1]
	v_pk_mul_f32 v[100:101], v[62:63], v[152:153] op_sel:[1,1] op_sel_hi:[0,1] neg_hi:[1,0]
	s_movk_i32 s62, 0xea00
	v_pk_fma_f32 v[62:63], v[62:63], v[152:153], v[100:101] op_sel_hi:[1,0,1]
	v_pk_mul_f32 v[100:101], v[66:67], v[150:151] op_sel:[1,1] op_sel_hi:[0,1] neg_hi:[1,0]
	s_movk_i32 s63, 0xe800
	v_pk_fma_f32 v[66:67], v[66:67], v[150:151], v[100:101] op_sel_hi:[1,0,1]
	v_pk_mul_f32 v[100:101], v[68:69], v[148:149] op_sel:[1,1] op_sel_hi:[0,1] neg_hi:[1,0]
	s_movk_i32 s66, 0xe600
	v_pk_fma_f32 v[68:69], v[68:69], v[148:149], v[100:101] op_sel_hi:[1,0,1]
	v_pk_mul_f32 v[100:101], v[70:71], v[146:147] op_sel:[1,1] op_sel_hi:[0,1] neg_hi:[1,0]
	s_movk_i32 s67, 0xe400
	v_pk_fma_f32 v[70:71], v[70:71], v[146:147], v[100:101] op_sel_hi:[1,0,1]
	v_pk_mul_f32 v[100:101], v[72:73], v[144:145] op_sel:[1,1] op_sel_hi:[0,1] neg_hi:[1,0]
	s_movk_i32 s68, 0xe200
	v_pk_fma_f32 v[72:73], v[72:73], v[144:145], v[100:101] op_sel_hi:[1,0,1]
	v_pk_mul_f32 v[100:101], v[90:91], v[142:143] op_sel:[1,1] op_sel_hi:[0,1] neg_hi:[1,0]
	s_movk_i32 s69, 0xe000
	v_pk_fma_f32 v[90:91], v[90:91], v[142:143], v[100:101] op_sel_hi:[1,0,1]
	v_pk_mul_f32 v[100:101], v[94:95], v[140:141] op_sel:[1,1] op_sel_hi:[0,1] neg_hi:[1,0]
	s_movk_i32 s74, 0xde00
	v_pk_fma_f32 v[94:95], v[94:95], v[140:141], v[100:101] op_sel_hi:[1,0,1]
	v_pk_mul_f32 v[100:101], v[98:99], v[138:139] op_sel:[1,1] op_sel_hi:[0,1] neg_hi:[1,0]
	s_movk_i32 s75, 0xdc00
	v_pk_fma_f32 v[144:145], v[98:99], v[138:139], v[100:101] op_sel_hi:[1,0,1]
	v_pk_mul_f32 v[98:99], v[96:97], v[136:137] op_sel:[1,1] op_sel_hi:[0,1] neg_hi:[1,0]
	s_movk_i32 s79, 0xda00
	v_pk_fma_f32 v[140:141], v[96:97], v[136:137], v[98:99] op_sel_hi:[1,0,1]
	v_pk_mul_f32 v[96:97], v[92:93], v[134:135] op_sel:[1,1] op_sel_hi:[0,1] neg_hi:[1,0]
	s_movk_i32 s56, 0xd800
	v_pk_fma_f32 v[138:139], v[92:93], v[134:135], v[96:97] op_sel_hi:[1,0,1]
	v_pk_mul_f32 v[92:93], v[88:89], v[132:133] op_sel:[1,1] op_sel_hi:[0,1] neg_hi:[1,0]
	s_mov_b32 s9, 0xbe94a031
	v_pk_fma_f32 v[136:137], v[88:89], v[132:133], v[92:93] op_sel_hi:[1,0,1]
	v_pk_mul_f32 v[88:89], v[86:87], v[130:131] op_sel:[1,1] op_sel_hi:[0,1] neg_hi:[1,0]
	s_mov_b32 s11, 0xbf0e39da
	v_pk_fma_f32 v[132:133], v[86:87], v[130:131], v[88:89] op_sel_hi:[1,0,1]
	v_pk_mul_f32 v[86:87], v[84:85], v[128:129] op_sel:[1,1] op_sel_hi:[0,1] neg_hi:[1,0]
	s_mov_b32 s15, 0xbf45e403
	v_pk_fma_f32 v[130:131], v[84:85], v[128:129], v[86:87] op_sel_hi:[1,0,1]
	v_pk_mul_f32 v[84:85], v[82:83], v[126:127] op_sel:[1,1] op_sel_hi:[0,1] neg_hi:[1,0]
	v_mov_b32_e32 v86, v19
	v_pk_fma_f32 v[92:93], v[82:83], v[126:127], v[84:85] op_sel_hi:[1,0,1]
	v_pk_mul_f32 v[82:83], v[80:81], v[124:125] op_sel:[1,1] op_sel_hi:[0,1] neg_hi:[1,0]
	v_pk_mul_f32 v[86:87], v[86:87], s[4:5] op_sel_hi:[0,1] neg_lo:[1,0]
	v_pk_fma_f32 v[96:97], v[80:81], v[124:125], v[82:83] op_sel_hi:[1,0,1]
	v_pk_mul_f32 v[80:81], v[78:79], v[116:117] op_sel:[1,1] op_sel_hi:[0,1] neg_hi:[1,0]
	v_pk_add_f32 v[88:89], v[96:97], v[58:59]
	v_pk_fma_f32 v[116:117], v[78:79], v[116:117], v[80:81] op_sel_hi:[1,0,1]
	v_pk_mul_f32 v[78:79], v[76:77], v[120:121] op_sel:[1,1] op_sel_hi:[0,1] neg_hi:[1,0]
	v_pk_fma_f32 v[86:87], v[16:17], s[44:45], v[86:87] op_sel_hi:[0,1,1]
	v_pk_fma_f32 v[120:121], v[76:77], v[120:121], v[78:79] op_sel_hi:[1,0,1]
	v_pk_mul_f32 v[76:77], v[74:75], v[122:123] op_sel:[1,1] op_sel_hi:[0,1] neg_hi:[1,0]
	v_pk_add_f32 v[78:79], v[92:93], v[8:9]
	v_pk_fma_f32 v[122:123], v[74:75], v[122:123], v[76:77] op_sel_hi:[1,0,1]
	v_pk_mul_f32 v[74:75], v[64:65], v[118:119] op_sel:[1,1] op_sel_hi:[0,1] neg_hi:[1,0]
	s_mov_b64 s[4:5], -1
	v_pk_fma_f32 v[124:125], v[64:65], v[118:119], v[74:75] op_sel_hi:[1,0,1]
	v_pk_mul_f32 v[64:65], v[56:57], v[114:115] op_sel:[1,1] op_sel_hi:[0,1] neg_hi:[1,0]
	s_mov_b32 s17, 0xbf61c598
	v_pk_fma_f32 v[126:127], v[56:57], v[114:115], v[64:65] op_sel_hi:[1,0,1]
	v_pk_mul_f32 v[56:57], v[54:55], v[112:113] op_sel:[1,1] op_sel_hi:[0,1] neg_hi:[1,0]
	v_pk_add_f32 v[118:119], v[126:127], v[70:71]
	v_pk_fma_f32 v[128:129], v[54:55], v[112:113], v[56:57] op_sel_hi:[1,0,1]
	v_pk_mul_f32 v[54:55], v[52:53], v[110:111] op_sel:[1,1] op_sel_hi:[0,1] neg_hi:[1,0]
	v_pk_add_f32 v[114:115], v[128:129], v[72:73]
	v_pk_fma_f32 v[134:135], v[52:53], v[110:111], v[54:55] op_sel_hi:[1,0,1]
	v_pk_mul_f32 v[52:53], v[50:51], v[108:109] op_sel:[1,1] op_sel_hi:[0,1] neg_hi:[1,0]
	v_pk_add_f32 v[64:65], v[134:135], v[90:91]
	v_pk_fma_f32 v[142:143], v[50:51], v[108:109], v[52:53] op_sel_hi:[1,0,1]
	v_pk_mul_f32 v[50:51], v[44:45], v[106:107] op_sel:[1,1] op_sel_hi:[0,1] neg_hi:[1,0]
	v_pk_add_f32 v[74:75], v[142:143], v[94:95]
	v_pk_fma_f32 v[146:147], v[44:45], v[106:107], v[50:51] op_sel_hi:[1,0,1]
	v_pk_mul_f32 v[44:45], v[42:43], v[104:105] op_sel:[1,1] op_sel_hi:[0,1] neg_hi:[1,0]
	v_pk_add_f32 v[76:77], v[146:147], v[144:145]
	v_pk_fma_f32 v[148:149], v[42:43], v[104:105], v[44:45] op_sel_hi:[1,0,1]
	v_pk_mul_f32 v[42:43], v[40:41], v[6:7] op_sel:[1,1] op_sel_hi:[0,1] neg_hi:[1,0]
	v_pk_add_f32 v[80:81], v[148:149], v[140:141]
	v_pk_fma_f32 v[150:151], v[40:41], v[6:7], v[42:43] op_sel_hi:[1,0,1]
	v_pk_mul_f32 v[6:7], v[38:39], v[4:5] op_sel:[1,1] op_sel_hi:[0,1] neg_hi:[1,0]
	v_pk_add_f32 v[104:105], v[150:151], v[138:139]
	v_pk_fma_f32 v[152:153], v[38:39], v[4:5], v[6:7] op_sel_hi:[1,0,1]
	v_pk_mul_f32 v[4:5], v[2:3], v[36:37] op_sel:[1,1] op_sel_hi:[1,0] neg_hi:[0,1]
	v_pk_add_f32 v[102:103], v[152:153], v[136:137]
	v_pk_fma_f32 v[154:155], v[36:37], v[2:3], v[4:5] op_sel_hi:[1,0,1]
	v_pk_fma_f32 v[156:157], v[34:35], 0, v[34:35] op_sel:[1,0,0] op_sel_hi:[0,0,1] neg_hi:[1,0,0]
	v_pk_add_f32 v[100:101], v[154:155], v[132:133]
	v_pk_add_f32 v[98:99], v[156:157], v[130:131]
	v_pk_add_f32 v[112:113], v[124:125], v[68:69]
	v_pk_add_f32 v[110:111], v[122:123], v[66:67]
	v_pk_add_f32 v[106:107], v[120:121], v[62:63]
	v_pk_add_f32 v[108:109], v[116:117], v[60:61]
	v_pk_add_f32 v[40:41], v[98:99], v[114:115]
	v_pk_add_f32 v[42:43], v[100:101], v[118:119]
	v_pk_add_f32 v[36:37], v[102:103], v[112:113]
	v_pk_add_f32 v[34:35], v[104:105], v[110:111]
	v_pk_add_f32 v[82:83], v[80:81], v[106:107]
	v_pk_add_f32 v[84:85], v[76:77], v[108:109]
	v_pk_add_f32 v[44:45], v[74:75], v[88:89]
	v_pk_add_f32 v[38:39], v[64:65], v[78:79]
	v_pk_add_f32 v[50:51], v[40:41], v[82:83]
	v_pk_add_f32 v[52:53], v[42:43], v[84:85]
	v_pk_add_f32 v[54:55], v[36:37], v[44:45]
	v_pk_add_f32 v[56:57], v[34:35], v[38:39]
	v_pk_add_f32 v[4:5], v[50:51], v[54:55]
	v_pk_add_f32 v[6:7], v[52:53], v[56:57]
	s_mov_b32 s19, 0xbf74fa0b
	v_pk_add_f32 v[2:3], v[4:5], v[6:7]
	s_movk_i32 s84, 0xce00
	v_pk_mul_f32 v[2:3], v[86:87], v[2:3]
	v_lshl_add_u64 v[86:87], v[14:15], 1, s[52:53]
	s_nop 0
	v_add_f32_e32 v2, v10, v2
	v_add_f32_e32 v10, v3, v2
	s_nop 0
	v_lshlrev_b32_e32 v2, 16, v25
	v_mul_f32_e32 v2, v198, v2
	v_fmac_f32_e32 v2, v197, v18
	v_fmac_f32_e32 v2, v199, v17
	v_add_f32_e32 v17, v200, v2
	v_lshl_add_u64 v[2:3], v[14:15], 2, s[64:65]
	v_mov_b32_e32 v18, v205
	s_movk_i32 s23, 0xfe00
	s_nop 0
	v_mul_f32_e32 v18, v13, v18
	v_fmac_f32_e32 v18, v201, v10
	v_mul_f32_e32 v10, v17, v18
	s_cbranch_vccz .LBB0_640
	v_bfe_u32 v15, v10, 16, 1
	s_movk_i32 s4, 0x7fff
	v_add3_u32 v15, v10, v15, s4
	global_store_short_d16_hi v[86:87], v15, off
	s_mov_b64 s[4:5], 0

.LBB0_646:
	s_or_b64 exec, exec, s[4:5]
	v_pk_add_f32 v[136:137], v[152:153], v[136:137] neg_lo:[0,1] neg_hi:[0,1]
	v_pk_add_f32 v[140:141], v[148:149], v[140:141] neg_lo:[0,1] neg_hi:[0,1]
	s_nop 0
	v_pk_mul_f32 v[152:153], v[30:31], v[136:137] op_sel:[0,1] op_sel_hi:[0,0] neg_lo:[0,1]
	v_pk_fma_f32 v[136:137], v[32:33], v[136:137], v[152:153] op_sel_hi:[0,1,1]
	v_mov_b32_e32 v33, v210
	v_pk_add_f32 v[72:73], v[128:129], v[72:73] neg_lo:[0,1] neg_hi:[0,1]
	v_pk_add_f32 v[70:71], v[126:127], v[70:71] neg_lo:[0,1] neg_hi:[0,1]
	v_pk_add_f32 v[90:91], v[134:135], v[90:91] neg_lo:[0,1] neg_hi:[0,1]
	v_xor_b32_e32 v134, 0x80000000, v73
	v_mov_b32_e32 v135, v72
	v_pk_mul_f32 v[148:149], v[46:47], v[140:141] op_sel:[0,1] op_sel_hi:[0,0] neg_lo:[0,1]
	v_pk_mul_f32 v[72:73], v[24:25], v[70:71] op_sel:[0,1] op_sel_hi:[0,0] neg_lo:[0,1]
	v_pk_add_f32 v[68:69], v[124:125], v[68:69] neg_lo:[0,1] neg_hi:[0,1]
	v_pk_fma_f32 v[140:141], v[46:47], v[140:141], v[148:149] op_sel_hi:[0,1,1]
	v_pk_fma_f32 v[148:149], v[26:27], v[70:71], v[72:73] op_sel_hi:[0,1,1] neg_lo:[1,0,0] neg_hi:[1,0,0]
	v_pk_add_f32 v[138:139], v[150:151], v[138:139] neg_lo:[0,1] neg_hi:[0,1]
	v_pk_add_f32 v[66:67], v[122:123], v[66:67] neg_lo:[0,1] neg_hi:[0,1]
	v_pk_mul_f32 v[150:151], v[48:49], v[138:139] op_sel:[0,1] op_sel_hi:[0,0] neg_lo:[0,1]
	v_pk_add_f32 v[62:63], v[120:121], v[62:63] neg_lo:[0,1] neg_hi:[0,1]
	v_pk_fma_f32 v[138:139], v[28:29], v[138:139], v[150:151] op_sel_hi:[0,1,1]
	v_pk_add_f32 v[144:145], v[146:147], v[144:145] neg_lo:[0,1] neg_hi:[0,1]
	v_pk_add_f32 v[132:133], v[154:155], v[132:133] neg_lo:[0,1] neg_hi:[0,1]
	v_pk_add_f32 v[60:61], v[116:117], v[60:61] neg_lo:[0,1] neg_hi:[0,1]
	v_pk_mul_f32 v[146:147], v[28:29], v[144:145] op_sel:[0,1] op_sel_hi:[0,0] neg_lo:[0,1]
	v_pk_mul_f32 v[154:155], v[26:27], v[132:133] op_sel:[0,1] op_sel_hi:[0,0] neg_lo:[0,1]
	v_pk_fma_f32 v[144:145], v[48:49], v[144:145], v[146:147] op_sel_hi:[0,1,1]
	v_pk_add_f32 v[94:95], v[142:143], v[94:95] neg_lo:[0,1] neg_hi:[0,1]
	v_pk_fma_f32 v[132:133], v[24:25], v[132:133], v[154:155] op_sel_hi:[0,1,1]
	v_pk_add_f32 v[8:9], v[92:93], v[8:9] neg_lo:[0,1] neg_hi:[0,1]
	v_pk_add_f32 v[130:131], v[156:157], v[130:131] neg_lo:[0,1] neg_hi:[0,1]
	v_pk_add_f32 v[92:93], v[132:133], v[148:149]
	v_xor_b32_e32 v18, 0x80000000, v19
	s_mov_b32 s4, s41
	s_mov_b32 s5, s40
	v_mov_b32_e32 v17, v16
	s_andn2_b64 vcc, exec, s[2:3]
	s_nop 0
	v_pk_mul_f32 v[70:71], v[32:33], v[68:69] op_sel:[0,1] op_sel_hi:[0,0] neg_lo:[0,1]
	v_pk_fma_f32 v[124:125], v[30:31], v[68:69], v[70:71] op_sel_hi:[0,1,1] neg_lo:[1,0,0] neg_hi:[1,0,0]
	v_pk_mul_f32 v[68:69], v[28:29], v[66:67] op_sel:[0,1] op_sel_hi:[0,0] neg_lo:[0,1]
	v_pk_fma_f32 v[150:151], v[48:49], v[66:67], v[68:69] op_sel_hi:[0,1,1] neg_lo:[1,0,0] neg_hi:[1,0,0]
	v_pk_mul_f32 v[66:67], v[46:47], v[62:63] op_sel:[0,1] op_sel_hi:[0,0] neg_lo:[0,1]
	v_pk_fma_f32 v[152:153], v[46:47], v[62:63], v[66:67] op_sel_hi:[0,1,1] neg_lo:[1,0,0] neg_hi:[1,0,0]
	v_xor_b32_e32 v62, 0x80000000, v61
	v_mov_b32_e32 v63, v60
	v_pk_mul_f32 v[48:49], v[48:49], v[62:63] op_sel_hi:[0,1]
	v_pk_fma_f32 v[154:155], v[28:29], v[60:61], v[48:49] op_sel_hi:[0,1,1] neg_lo:[1,0,0] neg_hi:[1,0,0]
	v_pk_add_f32 v[28:29], v[96:97], v[58:59] neg_lo:[0,1] neg_hi:[0,1]
	v_pk_mul_f32 v[142:143], v[32:33], v[94:95] op_sel:[0,1] op_sel_hi:[0,0] neg_lo:[0,1]
	v_pk_fma_f32 v[142:143], v[30:31], v[94:95], v[142:143] op_sel_hi:[0,1,1]
	v_pk_mul_f32 v[48:49], v[30:31], v[28:29] op_sel:[0,1] op_sel_hi:[0,0] neg_lo:[0,1]
	v_pk_mul_f32 v[94:95], v[24:25], v[90:91] op_sel:[0,1] op_sel_hi:[0,0] neg_lo:[0,1]
	v_pk_fma_f32 v[156:157], v[32:33], v[28:29], v[48:49] op_sel_hi:[0,1,1] neg_lo:[1,0,0] neg_hi:[1,0,0]
	v_pk_fma_f32 v[146:147], v[26:27], v[90:91], v[94:95] op_sel_hi:[0,1,1]
	v_pk_mul_f32 v[26:27], v[26:27], v[8:9] op_sel:[0,1] op_sel_hi:[0,0] neg_lo:[0,1]
	v_pk_fma_f32 v[158:159], v[24:25], v[8:9], v[26:27] op_sel_hi:[0,1,1] neg_lo:[1,0,0] neg_hi:[1,0,0]
	v_pk_add_f32 v[90:91], v[130:131], v[134:135]
	v_pk_add_f32 v[94:95], v[136:137], v[124:125]
	v_pk_add_f32 v[96:97], v[138:139], v[150:151]
	v_pk_add_f32 v[126:127], v[140:141], v[152:153]
	v_pk_add_f32 v[128:129], v[144:145], v[154:155]
	v_pk_add_f32 v[122:123], v[142:143], v[156:157]
	v_pk_add_f32 v[116:117], v[146:147], v[158:159]
	v_pk_add_f32 v[66:67], v[90:91], v[126:127]
	v_pk_add_f32 v[68:69], v[92:93], v[128:129]
	v_pk_add_f32 v[70:71], v[94:95], v[122:123]
	v_pk_add_f32 v[72:73], v[96:97], v[116:117]
	v_pk_add_f32 v[26:27], v[66:67], v[70:71]
	v_pk_add_f32 v[28:29], v[68:69], v[72:73]
	v_pk_mul_f32 v[48:49], v[18:19], s[4:5]
	v_pk_add_f32 v[8:9], v[26:27], v[28:29]
	v_pk_fma_f32 v[48:49], v[16:17], s[40:41], v[48:49]
	s_nop 0
	v_pk_mul_f32 v[8:9], v[48:49], v[8:9]
	s_nop 0
	v_add_f32_e32 v8, v8, v25
	v_add_f32_e32 v8, v9, v8
	v_lshlrev_b32_e32 v9, 16, v31
	v_mul_f32_e32 v9, v198, v9
	v_fmac_f32_e32 v9, v197, v10
	v_fmac_f32_e32 v9, v199, v15
	v_mul_f32_e32 v10, v13, v33
	v_add_f32_e32 v9, v200, v9
	v_fmac_f32_e32 v10, v201, v8
	v_mul_f32_e32 v8, v9, v10
	v_cndmask_b32_e64 v9, 0, 1, s[2:3]
	v_cmp_ne_u32_e64 s[4:5], 1, v9
	s_mov_b64 s[2:3], -1
	s_cbranch_vccnz .LBB0_648
	v_bfe_u32 v9, v8, 16, 1
	s_movk_i32 s2, 0x7fff
	v_add3_u32 v9, v8, v9, s2
	s_mov_b64 s[2:3], 0
	global_store_short_d16_hi v[86:87], v9, off offset:1024

.LBB0_654:
	s_or_b64 exec, exec, s[2:3]
	v_pk_add_f32 v[8:9], v[100:101], v[118:119] neg_lo:[0,1] neg_hi:[0,1]
	v_mov_b32_e32 v31, v30
	v_mov_b32_e32 v33, v32
	v_pk_mul_f32 v[24:25], v[30:31], v[8:9] op_sel:[0,1] op_sel_hi:[1,0] neg_lo:[0,1]
	v_mov_b32_e32 v47, v46
	v_pk_fma_f32 v[100:101], v[32:33], v[8:9], v[24:25]
	v_pk_add_f32 v[8:9], v[102:103], v[112:113] neg_lo:[0,1] neg_hi:[0,1]
	v_xor_b32_e32 v162, 0x80000000, v30
	v_pk_mul_f32 v[24:25], v[46:47], v[8:9] op_sel:[0,1] op_sel_hi:[1,0] neg_lo:[0,1]
	v_mov_b32_e32 v163, v162
	v_pk_fma_f32 v[102:103], v[46:47], v[8:9], v[24:25]
	v_pk_add_f32 v[8:9], v[104:105], v[110:111] neg_lo:[0,1] neg_hi:[0,1]
	v_xor_b32_e32 v48, 0x80000000, v46
	v_pk_mul_f32 v[24:25], v[32:33], v[8:9] op_sel:[0,1] op_sel_hi:[1,0] neg_lo:[0,1]
	v_mov_b32_e32 v49, v48
	v_pk_fma_f32 v[104:105], v[30:31], v[8:9], v[24:25]
	v_pk_add_f32 v[8:9], v[80:81], v[106:107] neg_lo:[0,1] neg_hi:[0,1]
	v_xor_b32_e32 v160, 0x80000000, v32
	v_xor_b32_e32 v106, 0x80000000, v9
	v_mov_b32_e32 v107, v8
	v_pk_add_f32 v[8:9], v[76:77], v[108:109] neg_lo:[0,1] neg_hi:[0,1]
	v_mov_b32_e32 v161, v160
	v_pk_mul_f32 v[24:25], v[32:33], v[8:9] op_sel:[0,1] op_sel_hi:[1,0] neg_lo:[0,1]
	v_pk_add_f32 v[98:99], v[98:99], v[114:115] neg_lo:[0,1] neg_hi:[0,1]
	v_pk_fma_f32 v[108:109], v[162:163], v[8:9], v[24:25]
	v_pk_add_f32 v[8:9], v[74:75], v[88:89] neg_lo:[0,1] neg_hi:[0,1]
	v_pk_add_f32 v[58:59], v[98:99], v[106:107]
	v_pk_mul_f32 v[24:25], v[46:47], v[8:9] op_sel:[0,1] op_sel_hi:[1,0] neg_lo:[0,1]
	v_pk_add_f32 v[60:61], v[100:101], v[108:109]
	v_pk_fma_f32 v[110:111], v[48:49], v[8:9], v[24:25]
	v_pk_add_f32 v[8:9], v[64:65], v[78:79] neg_lo:[0,1] neg_hi:[0,1]
	v_pk_add_f32 v[62:63], v[102:103], v[110:111]
	v_pk_mul_f32 v[24:25], v[30:31], v[8:9] op_sel:[0,1] op_sel_hi:[1,0] neg_lo:[0,1]
	s_mov_b32 s2, s77
	v_pk_fma_f32 v[112:113], v[160:161], v[8:9], v[24:25]
	s_mov_b32 s3, s76
	v_pk_add_f32 v[64:65], v[104:105], v[112:113]
	v_pk_add_f32 v[8:9], v[58:59], v[62:63]
	v_pk_add_f32 v[24:25], v[60:61], v[64:65]
	v_pk_mul_f32 v[76:77], v[18:19], s[2:3]
	v_pk_add_f32 v[74:75], v[8:9], v[24:25]
	v_pk_fma_f32 v[76:77], v[16:17], s[76:77], v[76:77]
	s_mov_b64 s[2:3], -1
	v_pk_mul_f32 v[74:75], v[76:77], v[74:75]
	s_nop 0
	v_add_f32_e32 v74, v74, v120
	v_add_f32_e32 v76, v75, v74
	s_nop 0
	v_lshlrev_b32_e32 v74, 16, v121
	v_mul_f32_e32 v74, v198, v74
	v_fmac_f32_e32 v74, v197, v10
	v_fmac_f32_e32 v74, v199, v15
	v_add_f32_e32 v10, v200, v74
	v_add_co_u32_e32 v74, vcc, 0x1000, v2
	s_nop 1
	v_addc_co_u32_e32 v75, vcc, 0, v3, vcc
	v_mov_b32_e32 v15, v215
	s_and_b64 vcc, exec, s[4:5]
	s_nop 0
	v_mul_f32_e32 v15, v13, v15
	v_fmac_f32_e32 v15, v201, v76
	v_mul_f32_e32 v10, v10, v15
	s_cbranch_vccnz .LBB0_656
	v_bfe_u32 v15, v10, 16, 1
	s_movk_i32 s2, 0x7fff
	v_add3_u32 v15, v10, v15, s2
	s_mov_b64 s[2:3], 0
	global_store_short_d16_hi v[86:87], v15, off offset:2048

.LBB0_662:
	s_or_b64 exec, exec, s[2:3]
	v_pk_add_f32 v[74:75], v[132:133], v[148:149] neg_lo:[0,1] neg_hi:[0,1]
	v_pk_add_f32 v[114:115], v[130:131], v[134:135] neg_lo:[0,1] neg_hi:[0,1]
	v_pk_mul_f32 v[76:77], v[30:31], v[74:75] op_sel:[0,1] op_sel_hi:[1,0] neg_lo:[0,1]
	s_mov_b32 s2, s9
	v_pk_fma_f32 v[118:119], v[32:33], v[74:75], v[76:77]
	v_pk_add_f32 v[74:75], v[136:137], v[124:125] neg_lo:[0,1] neg_hi:[0,1]
	s_mov_b32 s3, s8
	v_pk_mul_f32 v[76:77], v[46:47], v[74:75] op_sel:[0,1] op_sel_hi:[1,0] neg_lo:[0,1]
	s_nop 0
	v_pk_fma_f32 v[120:121], v[46:47], v[74:75], v[76:77]
	v_pk_add_f32 v[74:75], v[138:139], v[150:151] neg_lo:[0,1] neg_hi:[0,1]
	s_nop 0
	v_pk_mul_f32 v[76:77], v[32:33], v[74:75] op_sel:[0,1] op_sel_hi:[1,0] neg_lo:[0,1]
	s_nop 0
	v_pk_fma_f32 v[124:125], v[30:31], v[74:75], v[76:77]
	v_pk_add_f32 v[74:75], v[140:141], v[152:153] neg_lo:[0,1] neg_hi:[0,1]
	v_pk_mul_f32 v[140:141], v[18:19], s[2:3]
	v_xor_b32_e32 v130, 0x80000000, v75
	v_mov_b32_e32 v131, v74
	v_pk_add_f32 v[74:75], v[144:145], v[154:155] neg_lo:[0,1] neg_hi:[0,1]
	v_pk_fma_f32 v[140:141], v[16:17], s[8:9], v[140:141]
	v_pk_mul_f32 v[32:33], v[32:33], v[74:75] op_sel:[0,1] op_sel_hi:[1,0] neg_lo:[0,1]
	s_mov_b64 s[2:3], -1
	v_pk_fma_f32 v[132:133], v[162:163], v[74:75], v[32:33]
	v_pk_add_f32 v[32:33], v[142:143], v[156:157] neg_lo:[0,1] neg_hi:[0,1]
	v_pk_add_f32 v[76:77], v[118:119], v[132:133]
	v_pk_mul_f32 v[74:75], v[46:47], v[32:33] op_sel:[0,1] op_sel_hi:[1,0] neg_lo:[0,1]
	s_nop 0
	v_pk_fma_f32 v[134:135], v[48:49], v[32:33], v[74:75]
	v_pk_add_f32 v[32:33], v[146:147], v[158:159] neg_lo:[0,1] neg_hi:[0,1]
	v_pk_add_f32 v[78:79], v[120:121], v[134:135]
	v_pk_mul_f32 v[30:31], v[30:31], v[32:33] op_sel:[0,1] op_sel_hi:[1,0] neg_lo:[0,1]
	v_pk_add_f32 v[74:75], v[114:115], v[130:131]
	v_pk_fma_f32 v[136:137], v[160:161], v[32:33], v[30:31]
	v_pk_add_f32 v[30:31], v[74:75], v[78:79]
	v_pk_add_f32 v[80:81], v[124:125], v[136:137]
	s_nop 0
	v_pk_add_f32 v[32:33], v[76:77], v[80:81]
	s_nop 0
	v_pk_add_f32 v[138:139], v[30:31], v[32:33]
	s_nop 0
	v_pk_mul_f32 v[138:139], v[140:141], v[138:139]
	s_nop 0
	v_add_f32_e32 v88, v138, v88
	v_add_f32_e32 v138, v139, v88
	s_nop 0
	v_lshlrev_b32_e32 v88, 16, v89
	v_mul_f32_e32 v88, v198, v88
	v_fmac_f32_e32 v88, v197, v10
	v_fmac_f32_e32 v88, v199, v15
	v_add_f32_e32 v10, v200, v88
	v_add_co_u32_e32 v88, vcc, 0x1000, v2
	s_nop 1
	v_addc_co_u32_e32 v89, vcc, 0, v3, vcc
	v_mov_b32_e32 v15, v220
	s_and_b64 vcc, exec, s[4:5]
	s_nop 0
	v_mul_f32_e32 v15, v13, v15
	v_fmac_f32_e32 v15, v201, v138
	v_mul_f32_e32 v10, v10, v15
	s_cbranch_vccnz .LBB0_664
	v_bfe_u32 v15, v10, 16, 1
	s_movk_i32 s2, 0x7fff
	v_add3_u32 v15, v10, v15, s2
	s_mov_b64 s[2:3], 0
	global_store_short_d16_hi v[86:87], v15, off offset:3072

.LBB0_670:
	s_or_b64 exec, exec, s[2:3]
	v_pk_add_f32 v[82:83], v[40:41], v[82:83] neg_lo:[0,1] neg_hi:[0,1]
	v_pk_add_f32 v[40:41], v[42:43], v[84:85] neg_lo:[0,1] neg_hi:[0,1]
	v_pk_add_f32 v[36:37], v[36:37], v[44:45] neg_lo:[0,1] neg_hi:[0,1]
	v_pk_add_f32 v[34:35], v[34:35], v[38:39] neg_lo:[0,1] neg_hi:[0,1]
	v_xor_b32_e32 v86, 0x80000000, v37
	v_mov_b32_e32 v87, v36
	v_pk_mul_f32 v[42:43], v[46:47], v[40:41] op_sel:[0,1] op_sel_hi:[1,0] neg_lo:[0,1]
	v_pk_mul_f32 v[36:37], v[46:47], v[34:35] op_sel:[0,1] op_sel_hi:[1,0] neg_lo:[0,1]
	v_pk_fma_f32 v[84:85], v[46:47], v[40:41], v[42:43]
	v_pk_fma_f32 v[88:89], v[48:49], v[34:35], v[36:37]
	s_mov_b32 s2, s55
	s_mov_b32 s3, s54
	v_pk_add_f32 v[34:35], v[82:83], v[86:87]
	v_pk_add_f32 v[36:37], v[84:85], v[88:89]
	v_pk_mul_f32 v[40:41], v[18:19], s[2:3]
	v_pk_add_f32 v[38:39], v[34:35], v[36:37]
	v_pk_fma_f32 v[40:41], v[16:17], s[54:55], v[40:41]
	s_mov_b64 s[2:3], -1
	v_pk_mul_f32 v[38:39], v[40:41], v[38:39]
	s_nop 0
	v_add_f32_e32 v10, v38, v10
	s_nop 0
	v_lshlrev_b32_e32 v38, 16, v141
	v_mul_f32_e32 v38, v198, v38
	v_fmac_f32_e32 v38, v197, v140
	v_fmac_f32_e32 v38, v199, v15
	v_add_f32_e32 v15, v200, v38
	v_add_co_u32_e32 v38, vcc, 0x2000, v2
	v_add_f32_e32 v10, v39, v10
	s_nop 0
	v_addc_co_u32_e32 v39, vcc, 0, v3, vcc
	v_mov_b32_e32 v38, v225
	s_and_b64 vcc, exec, s[4:5]
	s_nop 0
	v_mul_f32_e32 v38, v13, v38
	v_fmac_f32_e32 v38, v201, v10
	v_mul_f32_e32 v10, v15, v38
	s_cbranch_vccnz .LBB0_672
	v_bfe_u32 v15, v10, 16, 1
	s_movk_i32 s2, 0x7fff
	v_add3_u32 v15, v10, v15, s2
	v_lshl_add_u64 v[38:39], v[138:139], 1, s[52:53]
	s_mov_b64 s[2:3], 0
	global_store_short_d16_hi v[38:39], v15, off

.LBB0_678:
	s_or_b64 exec, exec, s[2:3]
	s_nop 0
	v_lshlrev_b32_e32 v45, 16, v45
	v_mul_f32_e32 v45, v198, v45
	v_fmac_f32_e32 v45, v197, v44
	v_fmac_f32_e32 v45, v199, v15
	v_add_co_u32_e32 v44, vcc, 0x2000, v2
	v_add_f32_e32 v15, v200, v45
	s_nop 0
	v_addc_co_u32_e32 v45, vcc, 0, v3, vcc
	v_mov_b32_e32 v44, v230
	v_pk_add_f32 v[38:39], v[92:93], v[128:129] neg_lo:[0,1] neg_hi:[0,1]
	v_pk_add_f32 v[90:91], v[90:91], v[126:127] neg_lo:[0,1] neg_hi:[0,1]
	v_pk_mul_f32 v[40:41], v[46:47], v[38:39] op_sel:[0,1] op_sel_hi:[1,0] neg_lo:[0,1]
	s_mov_b32 s2, s81
	v_pk_fma_f32 v[92:93], v[46:47], v[38:39], v[40:41]
	v_pk_add_f32 v[38:39], v[94:95], v[122:123] neg_lo:[0,1] neg_hi:[0,1]
	s_mov_b32 s3, s80
	v_xor_b32_e32 v94, 0x80000000, v39
	v_mov_b32_e32 v95, v38
	v_pk_add_f32 v[38:39], v[96:97], v[116:117] neg_lo:[0,1] neg_hi:[0,1]
	v_pk_mul_f32 v[122:123], v[18:19], s[2:3]
	v_pk_mul_f32 v[40:41], v[46:47], v[38:39] op_sel:[0,1] op_sel_hi:[1,0] neg_lo:[0,1]
	v_pk_fma_f32 v[122:123], v[16:17], s[80:81], v[122:123]
	v_pk_fma_f32 v[96:97], v[48:49], v[38:39], v[40:41]
	v_pk_add_f32 v[38:39], v[90:91], v[94:95]
	v_pk_add_f32 v[40:41], v[92:93], v[96:97]
	s_mov_b64 s[2:3], -1
	v_pk_add_f32 v[116:117], v[38:39], v[40:41]
	s_and_b64 vcc, exec, s[4:5]
	v_pk_mul_f32 v[116:117], v[122:123], v[116:117]
	s_nop 0
	v_mul_f32_e32 v44, v13, v44
	v_add_f32_e32 v10, v116, v10
	v_add_f32_e32 v10, v117, v10
	v_fmac_f32_e32 v44, v201, v10
	v_mul_f32_e32 v10, v15, v44
	s_cbranch_vccnz .LBB0_680
	v_bfe_u32 v15, v10, 16, 1
	s_movk_i32 s2, 0x7fff
	v_add3_u32 v15, v10, v15, s2
	v_lshl_add_u64 v[42:43], v[42:43], 1, s[52:53]
	s_mov_b64 s[2:3], 0
	global_store_short_d16_hi v[42:43], v15, off

.LBB0_686:
	s_or_b64 exec, exec, s[2:3]
	v_pk_add_f32 v[42:43], v[100:101], v[108:109] neg_lo:[0,1] neg_hi:[0,1]
	v_pk_add_f32 v[98:99], v[98:99], v[106:107] neg_lo:[0,1] neg_hi:[0,1]
	v_pk_mul_f32 v[44:45], v[46:47], v[42:43] op_sel:[0,1] op_sel_hi:[1,0] neg_lo:[0,1]
	s_mov_b32 s2, s11
	v_pk_fma_f32 v[100:101], v[46:47], v[42:43], v[44:45]
	v_pk_add_f32 v[42:43], v[102:103], v[110:111] neg_lo:[0,1] neg_hi:[0,1]
	s_mov_b32 s3, s10
	v_xor_b32_e32 v102, 0x80000000, v43
	v_mov_b32_e32 v103, v42
	v_pk_add_f32 v[42:43], v[104:105], v[112:113] neg_lo:[0,1] neg_hi:[0,1]
	v_pk_mul_f32 v[108:109], v[18:19], s[2:3]
	v_pk_mul_f32 v[44:45], v[46:47], v[42:43] op_sel:[0,1] op_sel_hi:[1,0] neg_lo:[0,1]
	v_pk_fma_f32 v[108:109], v[16:17], s[10:11], v[108:109]
	v_pk_fma_f32 v[104:105], v[48:49], v[42:43], v[44:45]
	v_pk_add_f32 v[42:43], v[98:99], v[102:103]
	v_pk_add_f32 v[44:45], v[100:101], v[104:105]
	s_mov_b64 s[2:3], -1
	v_pk_add_f32 v[106:107], v[42:43], v[44:45]
	s_nop 0
	v_pk_mul_f32 v[106:107], v[108:109], v[106:107]
	s_nop 0
	v_add_f32_e32 v10, v106, v10
	s_nop 0
	v_lshlrev_b32_e32 v106, 16, v123
	v_mul_f32_e32 v106, v198, v106
	v_fmac_f32_e32 v106, v197, v122
	v_fmac_f32_e32 v106, v199, v15
	v_add_f32_e32 v15, v200, v106
	v_add_co_u32_e32 v106, vcc, 0x3000, v2
	v_add_f32_e32 v10, v107, v10
	s_nop 0
	v_addc_co_u32_e32 v107, vcc, 0, v3, vcc
	v_mov_b32_e32 v106, v235
	s_and_b64 vcc, exec, s[4:5]
	s_nop 0
	v_mul_f32_e32 v106, v13, v106
	v_fmac_f32_e32 v106, v201, v10
	v_mul_f32_e32 v10, v15, v106
	s_cbranch_vccnz .LBB0_688
	v_bfe_u32 v15, v10, 16, 1
	s_movk_i32 s2, 0x7fff
	v_add3_u32 v15, v10, v15, s2
	v_lshl_add_u64 v[106:107], v[116:117], 1, s[52:53]
	s_mov_b64 s[2:3], 0
	global_store_short_d16_hi v[106:107], v15, off

.LBB0_694:
	s_or_b64 exec, exec, s[2:3]
	v_pk_add_f32 v[108:109], v[118:119], v[132:133] neg_lo:[0,1] neg_hi:[0,1]
	v_pk_add_f32 v[112:113], v[120:121], v[134:135] neg_lo:[0,1] neg_hi:[0,1]
	v_pk_mul_f32 v[110:111], v[46:47], v[108:109] op_sel:[0,1] op_sel_hi:[1,0] neg_lo:[0,1]
	v_pk_add_f32 v[106:107], v[114:115], v[130:131] neg_lo:[0,1] neg_hi:[0,1]
	v_pk_fma_f32 v[108:109], v[46:47], v[108:109], v[110:111]
	v_xor_b32_e32 v110, 0x80000000, v113
	v_mov_b32_e32 v111, v112
	v_pk_add_f32 v[112:113], v[124:125], v[136:137] neg_lo:[0,1] neg_hi:[0,1]
	s_mov_b32 s2, s83
	v_pk_mul_f32 v[46:47], v[46:47], v[112:113] op_sel:[0,1] op_sel_hi:[1,0] neg_lo:[0,1]
	s_mov_b32 s3, s82
	v_pk_fma_f32 v[112:113], v[48:49], v[112:113], v[46:47]
	v_pk_add_f32 v[46:47], v[106:107], v[110:111]
	v_pk_add_f32 v[48:49], v[108:109], v[112:113]
	v_pk_mul_f32 v[118:119], v[18:19], s[2:3]
	v_pk_add_f32 v[114:115], v[46:47], v[48:49]
	v_pk_fma_f32 v[118:119], v[16:17], s[82:83], v[118:119]
	s_mov_b64 s[2:3], -1
	v_pk_mul_f32 v[114:115], v[118:119], v[114:115]
	s_nop 0
	v_add_f32_e32 v10, v114, v10
	s_nop 0
	v_lshlrev_b32_e32 v114, 16, v123
	v_mul_f32_e32 v114, v198, v114
	v_fmac_f32_e32 v114, v197, v122
	v_fmac_f32_e32 v114, v199, v15
	v_add_f32_e32 v15, v200, v114
	v_add_co_u32_e32 v114, vcc, 0x3000, v2
	v_add_f32_e32 v10, v115, v10
	s_nop 0
	v_addc_co_u32_e32 v115, vcc, 0, v3, vcc
	v_mov_b32_e32 v114, v240
	s_and_b64 vcc, exec, s[4:5]
	s_nop 0
	v_mul_f32_e32 v114, v13, v114
	v_fmac_f32_e32 v114, v201, v10
	v_mul_f32_e32 v10, v15, v114
	s_cbranch_vccnz .LBB0_696
	v_bfe_u32 v15, v10, 16, 1
	s_movk_i32 s2, 0x7fff
	v_add3_u32 v15, v10, v15, s2
	v_lshl_add_u64 v[114:115], v[116:117], 1, s[52:53]
	s_mov_b64 s[2:3], 0
	global_store_short_d16_hi v[114:115], v15, off

.LBB0_2730:
	s_or_b64 exec, exec, s[0:1]
	s_add_i32 s0, 0, 0x21000
	v_mov_b32_e32 v2, s0
	v_readlane_b32 s0, v251, 26
	v_mov_b32_e32 v92, v174
	s_waitcnt lgkmcnt(0)
	v_mov_b32_e32 v3, s0
	v_mov_b32_e32 v10, v164
	s_barrier
	ds_read_b128 v[6:9], v2
	ds_read_b128 v[2:5], v3
	v_mov_b32_e32 v60, v165
	v_mov_b32_e32 v34, v166
	v_mov_b32_e32 v62, v167
	v_mov_b32_e32 v32, v168
	v_mov_b32_e32 v64, v169
	v_mov_b32_e32 v38, v170
	v_mov_b32_e32 v66, v171
	v_mov_b32_e32 v10, v172
	v_pk_add_f32 v[68:69], v[14:15], v[42:43]
	v_pk_add_f32 v[14:15], v[14:15], v[42:43] neg_lo:[0,1] neg_hi:[0,1]
	s_nop 0
	v_mov_b32_e32 v13, v15
	v_mov_b32_e32 v10, v14
	v_mov_b32_e32 v42, v15
	v_mov_b32_e32 v43, v11
	v_pk_mul_f32 v[14:15], v[12:13], v[66:67] op_sel_hi:[1,0] neg_lo:[0,1] neg_hi:[0,1]
	v_pk_add_f32 v[70:71], v[18:19], v[52:53]
	v_pk_fma_f32 v[42:43], v[42:43], v[60:61], v[14:15] op_sel_hi:[1,0,1]
	v_pk_add_f32 v[14:15], v[16:17], v[48:49]
	v_pk_add_f32 v[48:49], v[16:17], v[48:49] neg_lo:[0,1] neg_hi:[0,1]
	v_mov_b32_e32 v17, v11
	v_mov_b32_e32 v13, v48
	v_mov_b32_e32 v16, v48
	v_pk_mul_f32 v[54:55], v[12:13], v[38:39] op_sel_hi:[1,0] neg_lo:[0,1] neg_hi:[0,1]
	v_mov_b32_e32 v13, v49
	v_pk_add_f32 v[18:19], v[18:19], v[52:53] neg_lo:[0,1] neg_hi:[0,1]
	v_pk_fma_f32 v[16:17], v[16:17], v[34:35], v[54:55] op_sel_hi:[1,0,1]
	v_mov_b32_e32 v54, v49
	v_mov_b32_e32 v55, v11
	v_pk_mul_f32 v[48:49], v[12:13], v[64:65] op_sel_hi:[1,0] neg_lo:[0,1] neg_hi:[0,1]
	v_mov_b32_e32 v13, v18
	v_pk_fma_f32 v[48:49], v[54:55], v[62:63], v[48:49] op_sel_hi:[1,0,1]
	v_mov_b32_e32 v52, v18
	v_mov_b32_e32 v53, v11
	v_pk_mul_f32 v[54:55], v[12:13], v[32:33] op_sel_hi:[1,0] neg_lo:[0,1] neg_hi:[0,1]
	v_mov_b32_e32 v13, v19
	v_pk_fma_f32 v[52:53], v[52:53], v[32:33], v[54:55] op_sel_hi:[1,0,1]
	v_mov_b32_e32 v54, v19
	v_mov_b32_e32 v55, v11
	v_pk_add_f32 v[18:19], v[20:21], v[50:51]
	v_pk_add_f32 v[20:21], v[20:21], v[50:51] neg_lo:[0,1] neg_hi:[0,1]
	v_pk_mul_f32 v[54:55], v[54:55], v[64:65] op_sel_hi:[1,0]
	v_mov_b32_e32 v50, v20
	v_mov_b32_e32 v51, v11
	v_pk_fma_f32 v[54:55], v[12:13], v[62:63], v[54:55] op_sel_hi:[1,0,1] neg_lo:[0,1,0] neg_hi:[0,1,0]
	v_pk_mul_f32 v[50:51], v[50:51], v[38:39] op_sel_hi:[1,0]
	v_mov_b32_e32 v13, v20
	v_pk_fma_f32 v[58:59], v[12:13], v[34:35], v[50:51] op_sel_hi:[1,0,1] neg_lo:[0,1,0] neg_hi:[0,1,0]
	v_mov_b32_e32 v50, v21
	v_mov_b32_e32 v51, v11
	v_pk_mul_f32 v[50:51], v[50:51], v[66:67] op_sel_hi:[1,0]
	v_mov_b32_e32 v13, v21
	v_pk_add_f32 v[20:21], v[24:25], v[46:47]
	v_pk_add_f32 v[24:25], v[24:25], v[46:47] neg_lo:[0,1] neg_hi:[0,1]
	v_pk_fma_f32 v[56:57], v[12:13], v[60:61], v[50:51] op_sel_hi:[1,0,1] neg_lo:[0,1,0] neg_hi:[0,1,0]
	v_xor_b32_e32 v73, 0x80000000, v24
	v_mov_b32_e32 v46, v25
	v_mov_b32_e32 v47, v11
	v_mov_b32_e32 v13, v25
	v_pk_add_f32 v[24:25], v[28:29], v[44:45]
	v_pk_add_f32 v[28:29], v[28:29], v[44:45] neg_lo:[0,1] neg_hi:[0,1]
	v_pk_mul_f32 v[46:47], v[46:47], v[66:67] op_sel_hi:[1,0] neg_lo:[0,1] neg_hi:[0,1]
	v_mov_b32_e32 v44, v28
	v_mov_b32_e32 v45, v11
	v_pk_fma_f32 v[74:75], v[12:13], v[60:61], v[46:47] op_sel_hi:[1,0,1] neg_lo:[0,1,0] neg_hi:[0,1,0]
	v_pk_mul_f32 v[44:45], v[44:45], v[38:39] op_sel_hi:[1,0] neg_lo:[0,1] neg_hi:[0,1]
	v_mov_b32_e32 v13, v28
	v_pk_fma_f32 v[76:77], v[12:13], v[34:35], v[44:45] op_sel_hi:[1,0,1] neg_lo:[0,1,0] neg_hi:[0,1,0]
	v_mov_b32_e32 v44, v29
	v_mov_b32_e32 v45, v11
	v_pk_mul_f32 v[44:45], v[44:45], v[64:65] op_sel_hi:[1,0] neg_lo:[0,1] neg_hi:[0,1]
	v_mov_b32_e32 v13, v29
	v_pk_add_f32 v[28:29], v[30:31], v[40:41]
	v_pk_add_f32 v[30:31], v[30:31], v[40:41] neg_lo:[0,1] neg_hi:[0,1]
	v_pk_fma_f32 v[78:79], v[12:13], v[62:63], v[44:45] op_sel_hi:[1,0,1] neg_lo:[0,1,0] neg_hi:[0,1,0]
	v_mov_b32_e32 v13, v30
	v_mov_b32_e32 v40, v30
	v_mov_b32_e32 v41, v11
	v_pk_mul_f32 v[44:45], v[12:13], v[32:33] op_sel_hi:[1,0] neg_lo:[0,1] neg_hi:[0,1]
	v_mov_b32_e32 v13, v31
	v_pk_fma_f32 v[80:81], v[40:41], v[32:33], v[44:45] op_sel_hi:[1,0,1] neg_lo:[0,1,0] neg_hi:[0,1,0]
	v_mov_b32_e32 v40, v31
	v_pk_mul_f32 v[30:31], v[12:13], v[64:65] op_sel_hi:[1,0] neg_lo:[0,1] neg_hi:[0,1]
	v_mov_b32_e32 v84, v11
	v_pk_fma_f32 v[62:63], v[40:41], v[62:63], v[30:31] op_sel_hi:[1,0,1] neg_lo:[0,1,0] neg_hi:[0,1,0]
	v_pk_add_f32 v[30:31], v[26:27], v[36:37]
	v_pk_add_f32 v[26:27], v[26:27], v[36:37] neg_lo:[0,1] neg_hi:[0,1]
	v_mov_b32_e32 v37, v11
	v_mov_b32_e32 v13, v26
	v_mov_b32_e32 v36, v26
	v_pk_mul_f32 v[40:41], v[12:13], v[38:39] op_sel_hi:[1,0] neg_lo:[0,1] neg_hi:[0,1]
	v_mov_b32_e32 v13, v27
	v_pk_fma_f32 v[64:65], v[36:37], v[34:35], v[40:41] op_sel_hi:[1,0,1] neg_lo:[0,1,0] neg_hi:[0,1,0]
	v_mov_b32_e32 v36, v27
	v_pk_mul_f32 v[26:27], v[12:13], v[66:67] op_sel_hi:[1,0] neg_lo:[0,1] neg_hi:[0,1]
	v_mov_b32_e32 v41, v11
	v_pk_fma_f32 v[66:67], v[36:37], v[60:61], v[26:27] op_sel_hi:[1,0,1] neg_lo:[0,1,0] neg_hi:[0,1,0]
	v_pk_add_f32 v[26:27], v[68:69], v[20:21] neg_lo:[0,1] neg_hi:[0,1]
	v_pk_add_f32 v[20:21], v[68:69], v[20:21]
	v_mov_b32_e32 v13, v27
	v_mov_b32_e32 v36, v26
	v_mov_b32_e32 v40, v27
	v_pk_mul_f32 v[26:27], v[12:13], v[38:39] op_sel_hi:[1,0] neg_lo:[0,1] neg_hi:[0,1]
	v_mov_b32_e32 v61, v11
	v_pk_fma_f32 v[44:45], v[40:41], v[34:35], v[26:27] op_sel_hi:[1,0,1]
	v_pk_add_f32 v[26:27], v[14:15], v[24:25] neg_lo:[0,1] neg_hi:[0,1]
	v_pk_add_f32 v[14:15], v[14:15], v[24:25]
	v_mov_b32_e32 v13, v26
	v_mov_b32_e32 v40, v26
	v_pk_mul_f32 v[46:47], v[12:13], v[32:33] op_sel_hi:[1,0] neg_lo:[0,1] neg_hi:[0,1]
	v_mov_b32_e32 v13, v27
	v_pk_fma_f32 v[50:51], v[40:41], v[32:33], v[46:47] op_sel_hi:[1,0,1]
	v_mov_b32_e32 v40, v27
	v_pk_mul_f32 v[40:41], v[40:41], v[38:39] op_sel_hi:[1,0]
	v_pk_add_f32 v[26:27], v[70:71], v[28:29] neg_lo:[0,1] neg_hi:[0,1]
	v_pk_fma_f32 v[82:83], v[12:13], v[34:35], v[40:41] op_sel_hi:[1,0,1] neg_lo:[0,1,0] neg_hi:[0,1,0]
	v_mov_b32_e32 v40, v27
	v_mov_b32_e32 v41, v11
	v_xor_b32_e32 v85, 0x80000000, v26
	v_pk_mul_f32 v[40:41], v[40:41], v[38:39] op_sel_hi:[1,0] neg_lo:[0,1] neg_hi:[0,1]
	v_mov_b32_e32 v13, v27
	v_pk_add_f32 v[26:27], v[18:19], v[30:31] neg_lo:[0,1] neg_hi:[0,1]
	v_pk_fma_f32 v[86:87], v[12:13], v[34:35], v[40:41] op_sel_hi:[1,0,1] neg_lo:[0,1,0] neg_hi:[0,1,0]
	v_mov_b32_e32 v13, v26
	v_mov_b32_e32 v40, v26
	v_mov_b32_e32 v41, v11
	v_pk_mul_f32 v[46:47], v[12:13], v[32:33] op_sel_hi:[1,0] neg_lo:[0,1] neg_hi:[0,1]
	v_mov_b32_e32 v13, v27
	v_pk_fma_f32 v[88:89], v[40:41], v[32:33], v[46:47] op_sel_hi:[1,0,1] neg_lo:[0,1,0] neg_hi:[0,1,0]
	v_mov_b32_e32 v40, v27
	v_pk_mul_f32 v[26:27], v[12:13], v[38:39] op_sel_hi:[1,0] neg_lo:[0,1] neg_hi:[0,1]
	v_pk_add_f32 v[24:25], v[70:71], v[28:29]
	v_pk_fma_f32 v[90:91], v[40:41], v[34:35], v[26:27] op_sel_hi:[1,0,1] neg_lo:[0,1,0] neg_hi:[0,1,0]
	v_pk_add_f32 v[26:27], v[20:21], v[24:25] neg_lo:[0,1] neg_hi:[0,1]
	v_pk_add_f32 v[18:19], v[18:19], v[30:31]
	v_mov_b32_e32 v13, v27
	v_mov_b32_e32 v28, v26
	v_pk_add_f32 v[20:21], v[20:21], v[24:25]
	v_mov_b32_e32 v24, v27
	v_mov_b32_e32 v25, v11
	v_pk_mul_f32 v[26:27], v[12:13], v[32:33] op_sel_hi:[1,0] neg_lo:[0,1] neg_hi:[0,1]
	v_mov_b32_e32 v29, v11
	v_pk_fma_f32 v[24:25], v[24:25], v[32:33], v[26:27] op_sel_hi:[1,0,1]
	v_pk_add_f32 v[26:27], v[14:15], v[18:19] neg_lo:[0,1] neg_hi:[0,1]
	v_pk_add_f32 v[14:15], v[14:15], v[18:19]
	v_mov_b32_e32 v13, v27
	v_xor_b32_e32 v41, 0x80000000, v26
	v_mov_b32_e32 v18, v27
	v_mov_b32_e32 v19, v11
	v_pk_mul_f32 v[26:27], v[12:13], v[32:33] op_sel_hi:[1,0] neg_lo:[0,1] neg_hi:[0,1]
	v_pk_add_f32 v[30:31], v[20:21], v[14:15]
	v_pk_fma_f32 v[18:19], v[18:19], v[32:33], v[26:27] op_sel_hi:[1,0,1] neg_lo:[0,1,0] neg_hi:[0,1,0]
	v_pk_add_f32 v[26:27], v[20:21], v[14:15] neg_lo:[0,1] neg_hi:[0,1]
	v_mov_b32_e32 v40, v11
	v_pk_add_f32 v[14:15], v[26:27], 0 neg_lo:[1,1] neg_hi:[1,1]
	v_mov_b32_e32 v60, v26
	v_mov_b32_e32 v14, v11
	v_pk_add_f32 v[26:27], v[24:25], v[18:19]
	v_pk_add_f32 v[18:19], v[24:25], v[18:19] neg_lo:[0,1] neg_hi:[0,1]
	v_pk_add_f32 v[46:47], v[60:61], v[14:15]
	v_pk_add_f32 v[20:21], v[60:61], v[14:15] neg_lo:[0,1] neg_hi:[0,1]
	v_pk_add_f32 v[14:15], v[28:29], v[40:41]
	v_pk_add_f32 v[28:29], v[28:29], v[40:41] neg_lo:[0,1] neg_hi:[0,1]
	v_pk_add_f32 v[60:61], v[14:15], v[26:27]
	v_pk_add_f32 v[26:27], v[14:15], v[26:27] neg_lo:[0,1] neg_hi:[0,1]
	v_pk_add_f32 v[40:41], v[28:29], v[18:19] op_sel:[0,1] op_sel_hi:[1,0] neg_hi:[0,1]
	v_pk_add_f32 v[14:15], v[28:29], v[18:19] op_sel:[0,1] op_sel_hi:[1,0] neg_lo:[0,1]
	v_pk_add_f32 v[18:19], v[36:37], v[84:85]
	v_pk_add_f32 v[28:29], v[36:37], v[84:85] neg_lo:[0,1] neg_hi:[0,1]
	v_pk_add_f32 v[36:37], v[44:45], v[86:87] neg_lo:[0,1] neg_hi:[0,1]
	v_pk_add_f32 v[24:25], v[44:45], v[86:87]
	v_pk_mul_f32 v[44:45], v[32:33], v[36:37] op_sel:[0,1] op_sel_hi:[0,0] neg_lo:[1,1] neg_hi:[1,0]
	v_pk_fma_f32 v[44:45], v[32:33], v[36:37], v[44:45] op_sel_hi:[0,1,1]
	v_pk_add_f32 v[36:37], v[50:51], v[88:89]
	v_pk_add_f32 v[50:51], v[50:51], v[88:89] neg_lo:[0,1] neg_hi:[0,1]
	v_pk_add_f32 v[70:71], v[82:83], v[90:91] neg_lo:[0,1] neg_hi:[0,1]
	v_xor_b32_e32 v69, 0x80000000, v50
	v_mov_b32_e32 v68, v51
	v_pk_add_f32 v[50:51], v[82:83], v[90:91]
	v_pk_mul_f32 v[82:83], v[32:33], v[70:71] op_sel:[0,1] op_sel_hi:[0,0] neg_lo:[1,1] neg_hi:[1,0]
	v_pk_fma_f32 v[70:71], v[32:33], v[70:71], v[82:83] op_sel_hi:[0,1,1] neg_lo:[1,0,0] neg_hi:[1,0,0]
	v_pk_add_f32 v[82:83], v[18:19], v[36:37]
	v_pk_add_f32 v[18:19], v[18:19], v[36:37] neg_lo:[0,1] neg_hi:[0,1]
	v_pk_add_f32 v[36:37], v[24:25], v[50:51]
	v_pk_add_f32 v[24:25], v[24:25], v[50:51] neg_lo:[0,1] neg_hi:[0,1]
	v_mov_b32_e32 v72, v11
	v_pk_add_f32 v[50:51], v[18:19], v[24:25] op_sel:[0,1] op_sel_hi:[1,0] neg_hi:[0,1]
	v_pk_add_f32 v[24:25], v[18:19], v[24:25] op_sel:[0,1] op_sel_hi:[1,0] neg_lo:[0,1]
	v_pk_add_f32 v[18:19], v[28:29], v[68:69]
	v_pk_add_f32 v[68:69], v[28:29], v[68:69] neg_lo:[0,1] neg_hi:[0,1]
	v_pk_add_f32 v[28:29], v[44:45], v[70:71]
	v_pk_add_f32 v[44:45], v[44:45], v[70:71] neg_lo:[0,1] neg_hi:[0,1]
	v_pk_add_f32 v[86:87], v[82:83], v[36:37]
	v_xor_b32_e32 v71, 0x80000000, v44
	v_mov_b32_e32 v70, v45
	v_pk_add_f32 v[36:37], v[82:83], v[36:37] neg_lo:[0,1] neg_hi:[0,1]
	v_pk_add_f32 v[82:83], v[18:19], v[28:29]
	v_pk_add_f32 v[28:29], v[18:19], v[28:29] neg_lo:[0,1] neg_hi:[0,1]
	v_pk_add_f32 v[44:45], v[68:69], v[70:71]
	v_pk_add_f32 v[18:19], v[68:69], v[70:71] neg_lo:[0,1] neg_hi:[0,1]
	v_pk_add_f32 v[68:69], v[10:11], v[72:73]
	v_pk_add_f32 v[70:71], v[10:11], v[72:73] neg_lo:[0,1] neg_hi:[0,1]
	v_pk_add_f32 v[72:73], v[42:43], v[74:75]
	v_pk_add_f32 v[42:43], v[42:43], v[74:75] neg_lo:[0,1] neg_hi:[0,1]
	v_add_f32_e32 v10, v30, v31
	v_pk_mul_f32 v[74:75], v[38:39], v[42:43] op_sel:[0,1] op_sel_hi:[0,0] neg_lo:[1,1] neg_hi:[1,0]
	v_pk_fma_f32 v[42:43], v[34:35], v[42:43], v[74:75] op_sel_hi:[0,1,1]
	v_pk_add_f32 v[74:75], v[16:17], v[76:77]
	v_pk_add_f32 v[16:17], v[16:17], v[76:77] neg_lo:[0,1] neg_hi:[0,1]
	v_lshl_add_u32 v13, v92, 3, 0
	v_pk_mul_f32 v[76:77], v[32:33], v[16:17] op_sel:[0,1] op_sel_hi:[0,0] neg_lo:[1,1] neg_hi:[1,0]
	v_pk_fma_f32 v[16:17], v[32:33], v[16:17], v[76:77] op_sel_hi:[0,1,1]
	v_pk_add_f32 v[76:77], v[48:49], v[78:79]
	v_pk_add_f32 v[48:49], v[48:49], v[78:79] neg_lo:[0,1] neg_hi:[0,1]
	s_nop 0
	v_pk_mul_f32 v[78:79], v[34:35], v[48:49] op_sel:[0,1] op_sel_hi:[0,0] neg_lo:[1,1] neg_hi:[1,0]
	v_pk_fma_f32 v[78:79], v[38:39], v[48:49], v[78:79] op_sel_hi:[0,1,1]
	v_pk_add_f32 v[48:49], v[52:53], v[80:81]
	v_pk_add_f32 v[52:53], v[52:53], v[80:81] neg_lo:[0,1] neg_hi:[0,1]
	s_nop 0
	v_xor_b32_e32 v81, 0x80000000, v52
	v_mov_b32_e32 v80, v53
	v_pk_add_f32 v[52:53], v[54:55], v[62:63]
	v_pk_add_f32 v[54:55], v[54:55], v[62:63] neg_lo:[0,1] neg_hi:[0,1]
	s_nop 0
	v_pk_mul_f32 v[62:63], v[34:35], v[54:55] op_sel:[0,1] op_sel_hi:[0,0] neg_lo:[1,1] neg_hi:[1,0]
	v_pk_fma_f32 v[62:63], v[38:39], v[54:55], v[62:63] op_sel_hi:[0,1,1] neg_lo:[1,0,0] neg_hi:[1,0,0]
	v_pk_add_f32 v[54:55], v[58:59], v[64:65]
	v_pk_add_f32 v[58:59], v[58:59], v[64:65] neg_lo:[0,1] neg_hi:[0,1]
	s_nop 0
	v_pk_mul_f32 v[64:65], v[32:33], v[58:59] op_sel:[0,1] op_sel_hi:[0,0] neg_lo:[1,1] neg_hi:[1,0]
	v_pk_fma_f32 v[58:59], v[32:33], v[58:59], v[64:65] op_sel_hi:[0,1,1] neg_lo:[1,0,0] neg_hi:[1,0,0]
	v_pk_add_f32 v[64:65], v[56:57], v[66:67]
	v_pk_add_f32 v[56:57], v[56:57], v[66:67] neg_lo:[0,1] neg_hi:[0,1]
	s_nop 0
	v_pk_mul_f32 v[38:39], v[38:39], v[56:57] op_sel:[0,1] op_sel_hi:[0,0] neg_lo:[1,1] neg_hi:[1,0]
	v_pk_fma_f32 v[56:57], v[34:35], v[56:57], v[38:39] op_sel_hi:[0,1,1] neg_lo:[1,0,0] neg_hi:[1,0,0]
	v_pk_add_f32 v[38:39], v[52:53], v[72:73]
	v_pk_add_f32 v[52:53], v[72:73], v[52:53] neg_lo:[0,1] neg_hi:[0,1]
	v_pk_add_f32 v[34:35], v[68:69], v[48:49]
	v_pk_mul_f32 v[66:67], v[32:33], v[52:53] op_sel:[0,1] op_sel_hi:[0,0] neg_lo:[1,1] neg_hi:[1,0]
	v_pk_fma_f32 v[52:53], v[32:33], v[52:53], v[66:67] op_sel_hi:[0,1,1]
	v_pk_add_f32 v[66:67], v[74:75], v[54:55]
	v_pk_add_f32 v[54:55], v[74:75], v[54:55] neg_lo:[0,1] neg_hi:[0,1]
	v_pk_add_f32 v[48:49], v[68:69], v[48:49] neg_lo:[0,1] neg_hi:[0,1]
	v_xor_b32_e32 v69, 0x80000000, v54
	v_mov_b32_e32 v68, v55
	v_pk_add_f32 v[54:55], v[76:77], v[64:65]
	v_pk_add_f32 v[64:65], v[76:77], v[64:65] neg_lo:[0,1] neg_hi:[0,1]
	s_nop 0
	v_pk_mul_f32 v[72:73], v[32:33], v[64:65] op_sel:[0,1] op_sel_hi:[0,0] neg_lo:[1,1] neg_hi:[1,0]
	v_pk_fma_f32 v[64:65], v[32:33], v[64:65], v[72:73] op_sel_hi:[0,1,1] neg_lo:[1,0,0] neg_hi:[1,0,0]
	v_pk_add_f32 v[72:73], v[34:35], v[66:67]
	v_pk_add_f32 v[34:35], v[34:35], v[66:67] neg_lo:[0,1] neg_hi:[0,1]
	v_pk_add_f32 v[66:67], v[38:39], v[54:55]
	v_pk_add_f32 v[38:39], v[38:39], v[54:55] neg_lo:[0,1] neg_hi:[0,1]
	v_pk_add_f32 v[76:77], v[72:73], v[66:67]
	v_pk_add_f32 v[54:55], v[72:73], v[66:67] neg_lo:[0,1] neg_hi:[0,1]
	v_pk_add_f32 v[66:67], v[34:35], v[38:39] op_sel:[0,1] op_sel_hi:[1,0] neg_hi:[0,1]
	v_pk_add_f32 v[38:39], v[34:35], v[38:39] op_sel:[0,1] op_sel_hi:[1,0] neg_lo:[0,1]
	v_pk_add_f32 v[34:35], v[48:49], v[68:69]
	v_pk_add_f32 v[68:69], v[48:49], v[68:69] neg_lo:[0,1] neg_hi:[0,1]
	v_pk_add_f32 v[48:49], v[52:53], v[64:65]
	v_pk_add_f32 v[52:53], v[52:53], v[64:65] neg_lo:[0,1] neg_hi:[0,1]
	v_pk_add_f32 v[72:73], v[34:35], v[48:49]
	v_pk_add_f32 v[48:49], v[34:35], v[48:49] neg_lo:[0,1] neg_hi:[0,1]
	v_pk_add_f32 v[74:75], v[68:69], v[52:53] op_sel:[0,1] op_sel_hi:[1,0] neg_hi:[0,1]
	v_pk_add_f32 v[34:35], v[68:69], v[52:53] op_sel:[0,1] op_sel_hi:[1,0] neg_lo:[0,1]
	v_pk_add_f32 v[68:69], v[62:63], v[42:43]
	v_pk_add_f32 v[42:43], v[42:43], v[62:63] neg_lo:[0,1] neg_hi:[0,1]
	v_pk_add_f32 v[52:53], v[70:71], v[80:81]
	v_pk_mul_f32 v[62:63], v[32:33], v[42:43] op_sel:[0,1] op_sel_hi:[0,0] neg_lo:[1,1] neg_hi:[1,0]
	v_pk_fma_f32 v[62:63], v[32:33], v[42:43], v[62:63] op_sel_hi:[0,1,1]
	v_pk_add_f32 v[42:43], v[16:17], v[58:59]
	v_pk_add_f32 v[16:17], v[16:17], v[58:59] neg_lo:[0,1] neg_hi:[0,1]
	v_pk_add_f32 v[64:65], v[70:71], v[80:81] neg_lo:[0,1] neg_hi:[0,1]
	v_xor_b32_e32 v59, 0x80000000, v16
	v_mov_b32_e32 v58, v17
	v_pk_add_f32 v[16:17], v[78:79], v[56:57]
	v_pk_add_f32 v[56:57], v[78:79], v[56:57] neg_lo:[0,1] neg_hi:[0,1]
	s_nop 0
	v_pk_mul_f32 v[70:71], v[32:33], v[56:57] op_sel:[0,1] op_sel_hi:[0,0] neg_lo:[1,1] neg_hi:[1,0]
	v_pk_fma_f32 v[32:33], v[32:33], v[56:57], v[70:71] op_sel_hi:[0,1,1] neg_lo:[1,0,0] neg_hi:[1,0,0]
	v_pk_add_f32 v[56:57], v[52:53], v[42:43]
	v_pk_add_f32 v[42:43], v[52:53], v[42:43] neg_lo:[0,1] neg_hi:[0,1]
	v_pk_add_f32 v[52:53], v[68:69], v[16:17]
	v_pk_add_f32 v[16:17], v[68:69], v[16:17] neg_lo:[0,1] neg_hi:[0,1]
	v_pk_add_f32 v[70:71], v[56:57], v[52:53]
	v_xor_b32_e32 v69, 0x80000000, v16
	v_mov_b32_e32 v68, v17
	v_pk_add_f32 v[56:57], v[56:57], v[52:53] neg_lo:[0,1] neg_hi:[0,1]
	v_pk_add_f32 v[16:17], v[64:65], v[58:59]
	v_pk_add_f32 v[52:53], v[62:63], v[32:33]
	v_pk_add_f32 v[32:33], v[62:63], v[32:33] neg_lo:[0,1] neg_hi:[0,1]
	v_pk_add_f32 v[58:59], v[64:65], v[58:59] neg_lo:[0,1] neg_hi:[0,1]
	v_pk_add_f32 v[64:65], v[16:17], v[52:53]
	v_pk_add_f32 v[52:53], v[16:17], v[52:53] neg_lo:[0,1] neg_hi:[0,1]
	v_mov_b64_e32 v[16:17], s[92:93]
	v_pk_add_f32 v[78:79], v[42:43], v[68:69]
	v_pk_add_f32 v[42:43], v[42:43], v[68:69] neg_lo:[0,1] neg_hi:[0,1]
	v_pk_add_f32 v[68:69], v[58:59], v[32:33] op_sel:[0,1] op_sel_hi:[1,0] neg_hi:[0,1]
	v_pk_add_f32 v[32:33], v[58:59], v[32:33] op_sel:[0,1] op_sel_hi:[1,0] neg_lo:[0,1]
	v_pk_fma_f32 v[58:59], v[10:11], s[42:43], v[16:17] op_sel_hi:[0,1,1]
	ds_write_b64 v13, v[58:59]
	v_pk_fma_f32 v[58:59], v[180:181], s[92:93], v[180:181] op_sel:[1,0,0] op_sel_hi:[0,1,1]
	v_pk_mul_f32 v[62:63], v[58:59], v[76:77] op_sel:[1,1] op_sel_hi:[0,1] neg_lo:[0,1]
	v_pk_fma_f32 v[62:63], v[58:59], v[76:77], v[62:63] op_sel_hi:[1,0,1]
	ds_write_b64 v13, v[62:63] offset:4224
	v_pk_mul_f32 v[62:63], v[180:181], v[58:59] op_sel:[1,1] op_sel_hi:[0,1] neg_lo:[0,1]
	v_pk_fma_f32 v[58:59], v[180:181], v[58:59], v[62:63] op_sel_hi:[1,0,1]
	s_nop 0
	v_pk_mul_f32 v[62:63], v[58:59], v[86:87] op_sel:[1,1] op_sel_hi:[0,1] neg_lo:[0,1]
	v_pk_fma_f32 v[62:63], v[58:59], v[86:87], v[62:63] op_sel_hi:[1,0,1]
	ds_write_b64 v13, v[62:63] offset:8448
	v_pk_mul_f32 v[62:63], v[180:181], v[58:59] op_sel:[1,1] op_sel_hi:[0,1] neg_lo:[0,1]
	v_pk_fma_f32 v[58:59], v[180:181], v[58:59], v[62:63] op_sel_hi:[1,0,1]
	s_nop 0
	v_pk_mul_f32 v[62:63], v[58:59], v[70:71] op_sel:[1,1] op_sel_hi:[0,1] neg_lo:[0,1]
	v_pk_fma_f32 v[62:63], v[58:59], v[70:71], v[62:63] op_sel_hi:[1,0,1]
	ds_write_b64 v13, v[62:63] offset:12672
	v_pk_mul_f32 v[62:63], v[180:181], v[58:59] op_sel:[1,1] op_sel_hi:[0,1] neg_lo:[0,1]
	v_pk_fma_f32 v[58:59], v[180:181], v[58:59], v[62:63] op_sel_hi:[1,0,1]
	s_nop 0
	v_pk_mul_f32 v[62:63], v[60:61], v[58:59] op_sel:[1,1] op_sel_hi:[1,0] neg_lo:[1,0]
	s_nop 0
	v_pk_fma_f32 v[60:61], v[60:61], v[58:59], v[62:63] op_sel_hi:[0,1,1]
	ds_write_b64 v13, v[60:61] offset:16896
	v_pk_mul_f32 v[60:61], v[180:181], v[58:59] op_sel:[1,1] op_sel_hi:[0,1] neg_lo:[0,1]
	v_pk_fma_f32 v[58:59], v[180:181], v[58:59], v[60:61] op_sel_hi:[1,0,1]
	s_nop 0
	v_pk_mul_f32 v[60:61], v[58:59], v[72:73] op_sel:[1,1] op_sel_hi:[0,1] neg_lo:[0,1]
	v_pk_fma_f32 v[60:61], v[58:59], v[72:73], v[60:61] op_sel_hi:[1,0,1]
	ds_write_b64 v13, v[60:61] offset:21120
	v_pk_mul_f32 v[60:61], v[180:181], v[58:59] op_sel:[1,1] op_sel_hi:[0,1] neg_lo:[0,1]
	v_pk_fma_f32 v[58:59], v[180:181], v[58:59], v[60:61] op_sel_hi:[1,0,1]
	s_nop 0
	v_pk_mul_f32 v[60:61], v[82:83], v[58:59] op_sel:[1,1] op_sel_hi:[1,0] neg_lo:[1,0]
	s_nop 0
	v_pk_fma_f32 v[60:61], v[82:83], v[58:59], v[60:61] op_sel_hi:[0,1,1]
	ds_write_b64 v13, v[60:61] offset:25344
	v_pk_mul_f32 v[60:61], v[180:181], v[58:59] op_sel:[1,1] op_sel_hi:[0,1] neg_lo:[0,1]
	v_pk_fma_f32 v[58:59], v[180:181], v[58:59], v[60:61] op_sel_hi:[1,0,1]
	s_nop 0
	v_pk_mul_f32 v[60:61], v[64:65], v[58:59] op_sel:[1,1] op_sel_hi:[1,0] neg_lo:[1,0]
	s_nop 0
	v_pk_fma_f32 v[60:61], v[64:65], v[58:59], v[60:61] op_sel_hi:[0,1,1]
	ds_write_b64 v13, v[60:61] offset:29568
	v_pk_mul_f32 v[60:61], v[180:181], v[58:59] op_sel:[1,1] op_sel_hi:[0,1] neg_lo:[0,1]
	v_pk_fma_f32 v[58:59], v[180:181], v[58:59], v[60:61] op_sel_hi:[1,0,1]
	s_nop 0
	v_pk_mul_f32 v[60:61], v[46:47], v[58:59] op_sel:[1,1] op_sel_hi:[1,0] neg_lo:[1,0]
	s_nop 0
	v_pk_fma_f32 v[46:47], v[46:47], v[58:59], v[60:61] op_sel_hi:[0,1,1]
	ds_write_b64 v13, v[46:47] offset:33792
	v_pk_mul_f32 v[46:47], v[180:181], v[58:59] op_sel:[1,1] op_sel_hi:[0,1] neg_lo:[0,1]
	v_pk_fma_f32 v[46:47], v[180:181], v[58:59], v[46:47] op_sel_hi:[1,0,1]
	s_nop 0
	v_pk_mul_f32 v[58:59], v[66:67], v[46:47] op_sel:[1,1] op_sel_hi:[1,0] neg_lo:[1,0]
	s_nop 0
	v_pk_fma_f32 v[58:59], v[66:67], v[46:47], v[58:59] op_sel_hi:[0,1,1]
	ds_write_b64 v13, v[58:59] offset:38016
	v_pk_mul_f32 v[58:59], v[180:181], v[46:47] op_sel:[1,1] op_sel_hi:[0,1] neg_lo:[0,1]
	v_pk_fma_f32 v[46:47], v[180:181], v[46:47], v[58:59] op_sel_hi:[1,0,1]
	s_nop 0
	v_pk_mul_f32 v[58:59], v[50:51], v[46:47] op_sel:[1,1] op_sel_hi:[1,0] neg_lo:[1,0]
	s_nop 0
	v_pk_fma_f32 v[50:51], v[50:51], v[46:47], v[58:59] op_sel_hi:[0,1,1]
	ds_write_b64 v13, v[50:51] offset:42240
	v_pk_mul_f32 v[50:51], v[180:181], v[46:47] op_sel:[1,1] op_sel_hi:[0,1] neg_lo:[0,1]
	v_pk_fma_f32 v[46:47], v[180:181], v[46:47], v[50:51] op_sel_hi:[1,0,1]
	s_nop 0
	v_pk_mul_f32 v[50:51], v[78:79], v[46:47] op_sel:[1,1] op_sel_hi:[1,0] neg_lo:[1,0]
	s_nop 0
	v_pk_fma_f32 v[50:51], v[78:79], v[46:47], v[50:51] op_sel_hi:[0,1,1]
	ds_write_b64 v13, v[50:51] offset:46464
	v_pk_mul_f32 v[50:51], v[180:181], v[46:47] op_sel:[1,1] op_sel_hi:[0,1] neg_lo:[0,1]
	v_pk_fma_f32 v[46:47], v[180:181], v[46:47], v[50:51] op_sel_hi:[1,0,1]
	s_nop 0
	v_pk_mul_f32 v[50:51], v[40:41], v[46:47] op_sel:[1,1] op_sel_hi:[1,0] neg_lo:[1,0]
	s_nop 0
	v_pk_fma_f32 v[40:41], v[40:41], v[46:47], v[50:51] op_sel_hi:[0,1,1]
	ds_write_b64 v13, v[40:41] offset:50688
	v_pk_mul_f32 v[40:41], v[180:181], v[46:47] op_sel:[1,1] op_sel_hi:[0,1] neg_lo:[0,1]
	v_pk_fma_f32 v[40:41], v[180:181], v[46:47], v[40:41] op_sel_hi:[1,0,1]
	s_nop 0
	v_pk_mul_f32 v[46:47], v[74:75], v[40:41] op_sel:[1,1] op_sel_hi:[1,0] neg_lo:[1,0]
	s_nop 0
	v_pk_fma_f32 v[46:47], v[74:75], v[40:41], v[46:47] op_sel_hi:[0,1,1]
	ds_write_b64 v13, v[46:47] offset:54912
	v_pk_mul_f32 v[46:47], v[180:181], v[40:41] op_sel:[1,1] op_sel_hi:[0,1] neg_lo:[0,1]
	v_pk_fma_f32 v[40:41], v[180:181], v[40:41], v[46:47] op_sel_hi:[1,0,1]
	s_nop 0
	v_pk_mul_f32 v[46:47], v[44:45], v[40:41] op_sel:[1,1] op_sel_hi:[1,0] neg_lo:[1,0]
	s_nop 0
	v_pk_fma_f32 v[44:45], v[44:45], v[40:41], v[46:47] op_sel_hi:[0,1,1]
	ds_write_b64 v13, v[44:45] offset:59136
	v_pk_mul_f32 v[44:45], v[180:181], v[40:41] op_sel:[1,1] op_sel_hi:[0,1] neg_lo:[0,1]
	v_pk_fma_f32 v[40:41], v[180:181], v[40:41], v[44:45] op_sel_hi:[1,0,1]
	s_nop 0
	v_pk_mul_f32 v[44:45], v[68:69], v[40:41] op_sel:[1,1] op_sel_hi:[1,0] neg_lo:[1,0]
	s_nop 0
	v_pk_fma_f32 v[44:45], v[68:69], v[40:41], v[44:45] op_sel_hi:[0,1,1]
	ds_write_b64 v13, v[44:45] offset:63360
	v_pk_mul_f32 v[44:45], v[180:181], v[40:41] op_sel:[1,1] op_sel_hi:[0,1] neg_lo:[0,1]
	v_pk_fma_f32 v[40:41], v[180:181], v[40:41], v[44:45] op_sel_hi:[1,0,1]
	s_mov_b32 s46, s43
	v_sub_f32_e32 v10, v30, v31
	v_pk_mul_f32 v[30:31], v[40:41], s[46:47]
	s_nop 0
	v_pk_fma_f32 v[30:31], v[10:11], v[40:41], v[30:31] op_sel:[0,0,1] op_sel_hi:[0,1,0]
	v_add_u32_e32 v10, 0x10800, v13
	ds_write_b64 v10, v[30:31]
	v_pk_mul_f32 v[30:31], v[180:181], v[40:41] op_sel:[1,1] op_sel_hi:[0,1] neg_lo:[0,1]
	v_pk_fma_f32 v[30:31], v[180:181], v[40:41], v[30:31] op_sel_hi:[1,0,1]
	s_nop 0
	v_pk_mul_f32 v[40:41], v[54:55], v[30:31] op_sel:[1,1] op_sel_hi:[1,0] neg_lo:[1,0]
	v_add_u32_e32 v10, 0x11880, v13
	v_pk_fma_f32 v[40:41], v[54:55], v[30:31], v[40:41] op_sel_hi:[0,1,1]
	ds_write_b64 v10, v[40:41]
	v_pk_mul_f32 v[40:41], v[180:181], v[30:31] op_sel:[1,1] op_sel_hi:[0,1] neg_lo:[0,1]
	v_pk_fma_f32 v[30:31], v[180:181], v[30:31], v[40:41] op_sel_hi:[1,0,1]
	s_nop 0
	v_pk_mul_f32 v[40:41], v[36:37], v[30:31] op_sel:[1,1] op_sel_hi:[1,0] neg_lo:[1,0]
	v_add_u32_e32 v10, 0x12900, v13
	v_pk_fma_f32 v[36:37], v[36:37], v[30:31], v[40:41] op_sel_hi:[0,1,1]
	ds_write_b64 v10, v[36:37]
	v_pk_mul_f32 v[36:37], v[180:181], v[30:31] op_sel:[1,1] op_sel_hi:[0,1] neg_lo:[0,1]
	v_pk_fma_f32 v[30:31], v[180:181], v[30:31], v[36:37] op_sel_hi:[1,0,1]
	s_nop 0
	v_pk_mul_f32 v[36:37], v[56:57], v[30:31] op_sel:[1,1] op_sel_hi:[1,0] neg_lo:[1,0]
	v_add_u32_e32 v10, 0x13980, v13
	v_pk_fma_f32 v[36:37], v[56:57], v[30:31], v[36:37] op_sel_hi:[0,1,1]
	ds_write_b64 v10, v[36:37]
	v_pk_mul_f32 v[36:37], v[180:181], v[30:31] op_sel:[1,1] op_sel_hi:[0,1] neg_lo:[0,1]
	v_pk_fma_f32 v[30:31], v[180:181], v[30:31], v[36:37] op_sel_hi:[1,0,1]
	s_nop 0
	v_pk_mul_f32 v[36:37], v[26:27], v[30:31] op_sel:[1,1] op_sel_hi:[1,0] neg_lo:[1,0]
	v_add_u32_e32 v10, 0x14a00, v13
	v_pk_fma_f32 v[26:27], v[26:27], v[30:31], v[36:37] op_sel_hi:[0,1,1]
	ds_write_b64 v10, v[26:27]
	v_pk_mul_f32 v[26:27], v[180:181], v[30:31] op_sel:[1,1] op_sel_hi:[0,1] neg_lo:[0,1]
	v_pk_fma_f32 v[26:27], v[180:181], v[30:31], v[26:27] op_sel_hi:[1,0,1]
	s_nop 0
	v_pk_mul_f32 v[30:31], v[48:49], v[26:27] op_sel:[1,1] op_sel_hi:[1,0] neg_lo:[1,0]
	v_add_u32_e32 v10, 0x15a80, v13
	v_pk_fma_f32 v[30:31], v[48:49], v[26:27], v[30:31] op_sel_hi:[0,1,1]
	ds_write_b64 v10, v[30:31]
	v_pk_mul_f32 v[30:31], v[180:181], v[26:27] op_sel:[1,1] op_sel_hi:[0,1] neg_lo:[0,1]
	v_pk_fma_f32 v[26:27], v[180:181], v[26:27], v[30:31] op_sel_hi:[1,0,1]
	s_nop 0
	v_pk_mul_f32 v[30:31], v[28:29], v[26:27] op_sel:[1,1] op_sel_hi:[1,0] neg_lo:[1,0]
	v_add_u32_e32 v10, 0x16b00, v13
	v_pk_fma_f32 v[28:29], v[28:29], v[26:27], v[30:31] op_sel_hi:[0,1,1]
	ds_write_b64 v10, v[28:29]
	v_pk_mul_f32 v[28:29], v[180:181], v[26:27] op_sel:[1,1] op_sel_hi:[0,1] neg_lo:[0,1]
	v_pk_fma_f32 v[26:27], v[180:181], v[26:27], v[28:29] op_sel_hi:[1,0,1]
	s_nop 0
	v_pk_mul_f32 v[28:29], v[52:53], v[26:27] op_sel:[1,1] op_sel_hi:[1,0] neg_lo:[1,0]
	v_add_u32_e32 v10, 0x17b80, v13
	v_pk_fma_f32 v[28:29], v[52:53], v[26:27], v[28:29] op_sel_hi:[0,1,1]
	ds_write_b64 v10, v[28:29]
	v_pk_mul_f32 v[28:29], v[180:181], v[26:27] op_sel:[1,1] op_sel_hi:[0,1] neg_lo:[0,1]
	v_pk_fma_f32 v[26:27], v[180:181], v[26:27], v[28:29] op_sel_hi:[1,0,1]
	s_nop 0
	v_pk_mul_f32 v[28:29], v[20:21], v[26:27] op_sel:[1,1] op_sel_hi:[1,0] neg_lo:[1,0]
	v_add_u32_e32 v10, 0x18c00, v13
	v_pk_fma_f32 v[20:21], v[20:21], v[26:27], v[28:29] op_sel_hi:[0,1,1]
	ds_write_b64 v10, v[20:21]
	v_pk_mul_f32 v[20:21], v[180:181], v[26:27] op_sel:[1,1] op_sel_hi:[0,1] neg_lo:[0,1]
	v_pk_fma_f32 v[20:21], v[180:181], v[26:27], v[20:21] op_sel_hi:[1,0,1]
	s_nop 0
	v_pk_mul_f32 v[26:27], v[38:39], v[20:21] op_sel:[1,1] op_sel_hi:[1,0] neg_lo:[1,0]
	v_add_u32_e32 v10, 0x19c80, v13
	v_pk_fma_f32 v[26:27], v[38:39], v[20:21], v[26:27] op_sel_hi:[0,1,1]
	ds_write_b64 v10, v[26:27]
	v_pk_mul_f32 v[26:27], v[180:181], v[20:21] op_sel:[1,1] op_sel_hi:[0,1] neg_lo:[0,1]
	v_pk_fma_f32 v[20:21], v[180:181], v[20:21], v[26:27] op_sel_hi:[1,0,1]
	s_nop 0
	v_pk_mul_f32 v[26:27], v[24:25], v[20:21] op_sel:[1,1] op_sel_hi:[1,0] neg_lo:[1,0]
	v_add_u32_e32 v10, 0x1ad00, v13
	v_pk_fma_f32 v[24:25], v[24:25], v[20:21], v[26:27] op_sel_hi:[0,1,1]
	ds_write_b64 v10, v[24:25]
	v_pk_mul_f32 v[24:25], v[180:181], v[20:21] op_sel:[1,1] op_sel_hi:[0,1] neg_lo:[0,1]
	v_pk_fma_f32 v[20:21], v[180:181], v[20:21], v[24:25] op_sel_hi:[1,0,1]
	s_nop 0
	v_pk_mul_f32 v[24:25], v[42:43], v[20:21] op_sel:[1,1] op_sel_hi:[1,0] neg_lo:[1,0]
	v_add_u32_e32 v10, 0x1bd80, v13
	v_pk_fma_f32 v[24:25], v[42:43], v[20:21], v[24:25] op_sel_hi:[0,1,1]
	ds_write_b64 v10, v[24:25]
	v_pk_mul_f32 v[24:25], v[180:181], v[20:21] op_sel:[1,1] op_sel_hi:[0,1] neg_lo:[0,1]
	v_pk_fma_f32 v[20:21], v[180:181], v[20:21], v[24:25] op_sel_hi:[1,0,1]
	s_nop 0
	v_pk_mul_f32 v[24:25], v[14:15], v[20:21] op_sel:[1,1] op_sel_hi:[1,0] neg_lo:[1,0]
	v_add_u32_e32 v10, 0x1ce00, v13
	v_pk_fma_f32 v[14:15], v[14:15], v[20:21], v[24:25] op_sel_hi:[0,1,1]
	ds_write_b64 v10, v[14:15]
	v_pk_mul_f32 v[14:15], v[180:181], v[20:21] op_sel:[1,1] op_sel_hi:[0,1] neg_lo:[0,1]
	v_pk_fma_f32 v[14:15], v[180:181], v[20:21], v[14:15] op_sel_hi:[1,0,1]
	s_nop 0
	v_pk_mul_f32 v[20:21], v[34:35], v[14:15] op_sel:[1,1] op_sel_hi:[1,0] neg_lo:[1,0]
	v_add_u32_e32 v10, 0x1de80, v13
	v_pk_fma_f32 v[20:21], v[34:35], v[14:15], v[20:21] op_sel_hi:[0,1,1]
	ds_write_b64 v10, v[20:21]
	v_pk_mul_f32 v[20:21], v[180:181], v[14:15] op_sel:[1,1] op_sel_hi:[0,1] neg_lo:[0,1]
	v_pk_fma_f32 v[14:15], v[180:181], v[14:15], v[20:21] op_sel_hi:[1,0,1]
	s_nop 0
	v_pk_mul_f32 v[20:21], v[18:19], v[14:15] op_sel:[1,1] op_sel_hi:[1,0] neg_lo:[1,0]
	v_add_u32_e32 v10, 0x1ef00, v13
	v_pk_fma_f32 v[18:19], v[18:19], v[14:15], v[20:21] op_sel_hi:[0,1,1]
	ds_write_b64 v10, v[18:19]
	v_pk_mul_f32 v[18:19], v[180:181], v[14:15] op_sel:[1,1] op_sel_hi:[0,1] neg_lo:[0,1]
	v_pk_fma_f32 v[14:15], v[180:181], v[14:15], v[18:19] op_sel_hi:[1,0,1]
	s_nop 0
	v_pk_mul_f32 v[18:19], v[32:33], v[14:15] op_sel:[1,1] op_sel_hi:[1,0] neg_lo:[1,0]
	v_add_u32_e32 v10, 0x1ff80, v13
	v_pk_fma_f32 v[14:15], v[32:33], v[14:15], v[18:19] op_sel_hi:[0,1,1]
	ds_write_b64 v10, v[14:15]
	v_mov_b32_e32 v10, v176
	v_mov_b32_e32 v13, v173
	s_waitcnt lgkmcnt(0)
	s_barrier
	v_mov_b32_e32 v14, v182
	v_xad_u32 v30, v13, 3, v10
	v_lshl_add_u32 v73, v30, 3, 0
	v_xad_u32 v30, v13, 4, v10
	v_lshl_add_u32 v72, v30, 3, 0
	v_xad_u32 v30, v13, 5, v10
	v_lshl_add_u32 v71, v30, 3, 0
	v_xad_u32 v30, v13, 6, v10
	v_lshl_add_u32 v70, v30, 3, 0
	v_xad_u32 v30, v13, 7, v10
	v_lshl_add_u32 v69, v30, 3, 0
	v_xad_u32 v30, v13, 8, v10
	v_lshl_add_u32 v30, v30, 3, 0
	v_add_u32_e32 v68, 0x800, v30
	v_xad_u32 v30, v13, 9, v10
	v_lshl_add_u32 v30, v30, 3, 0
	v_add_u32_e32 v67, 0x800, v30
	v_xad_u32 v30, v13, 10, v10
	v_lshl_add_u32 v30, v30, 3, 0
	v_add_u32_e32 v66, 0x800, v30
	v_xad_u32 v30, v13, 11, v10
	v_lshl_add_u32 v30, v30, 3, 0
	v_add_u32_e32 v18, v13, v10
	v_add_u32_e32 v65, 0x800, v30
	v_xad_u32 v30, v13, 12, v10
	v_mov_b32_e32 v15, v183
	v_lshl_add_u32 v76, v18, 3, 0
	v_lshl_add_u32 v30, v30, 3, 0
	ds_read2_b64 v[18:21], v76 offset1:16
	ds_read2_b64 v[40:43], v68 offset1:16
	v_add_u32_e32 v64, 0x800, v30
	v_xad_u32 v30, v13, 13, v10
	v_xad_u32 v22, v13, 1, v10
	v_lshl_add_u32 v30, v30, 3, 0
	v_lshl_add_u32 v75, v22, 3, 0
	v_xad_u32 v26, v13, 2, v10
	v_add_u32_e32 v63, 0x800, v30
	v_xad_u32 v30, v13, 14, v10
	v_xad_u32 v10, v13, 15, v10
	ds_read2_b64 v[22:25], v75 offset0:32 offset1:48
	ds_read2_b64 v[48:51], v67 offset0:32 offset1:48
	v_lshl_add_u32 v30, v30, 3, 0
	v_lshl_add_u32 v10, v10, 3, 0
	v_lshl_add_u32 v74, v26, 3, 0
	v_add_u32_e32 v62, 0x800, v30
	v_add_u32_e32 v13, 0x800, v10
	v_mov_b32_e32 v10, v164
	ds_read2_b64 v[26:29], v74 offset0:64 offset1:80
	ds_read2_b64 v[58:61], v73 offset0:96 offset1:112
	ds_read2_b64 v[78:81], v72 offset0:128 offset1:144
	ds_read2_b64 v[82:85], v71 offset0:160 offset1:176
	ds_read2_b64 v[86:89], v70 offset0:192 offset1:208
	ds_read2_b64 v[90:93], v69 offset0:224 offset1:240
	ds_read2_b64 v[54:57], v66 offset0:64 offset1:80
	ds_read2_b64 v[94:97], v65 offset0:96 offset1:112
	ds_read2_b64 v[98:101], v64 offset0:128 offset1:144
	ds_read2_b64 v[102:105], v63 offset0:160 offset1:176
	ds_read2_b64 v[106:109], v62 offset0:192 offset1:208
	ds_read2_b64 v[110:113], v13 offset0:224 offset1:240
	s_waitcnt lgkmcnt(14)
	v_pk_add_f32 v[114:115], v[18:19], v[40:41]
	v_pk_add_f32 v[40:41], v[18:19], v[40:41] neg_lo:[0,1] neg_hi:[0,1]
	v_pk_add_f32 v[18:19], v[20:21], v[42:43]
	v_pk_add_f32 v[20:21], v[20:21], v[42:43] neg_lo:[0,1] neg_hi:[0,1]
	v_mov_b32_e32 v30, v165
	v_mov_b32_e32 v32, v166
	v_mov_b32_e32 v34, v167
	v_mov_b32_e32 v10, v168
	v_mov_b32_e32 v38, v169
	v_mov_b32_e32 v36, v170
	v_mov_b32_e32 v46, v171
	v_mov_b32_e32 v31, v172
	v_pk_mul_f32 v[42:43], v[20:21], v[46:47] op_sel:[1,0] op_sel_hi:[0,0] neg_lo:[1,1] neg_hi:[0,1]
	s_mov_b32 s14, s43
	v_pk_fma_f32 v[44:45], v[20:21], v[30:31], v[42:43] op_sel_hi:[1,0,1]
	s_waitcnt lgkmcnt(12)
	v_pk_add_f32 v[20:21], v[22:23], v[48:49]
	v_pk_add_f32 v[22:23], v[22:23], v[48:49] neg_lo:[0,1] neg_hi:[0,1]
	s_mov_b32 s15, s42
	v_pk_mul_f32 v[42:43], v[22:23], v[36:37] op_sel:[1,0] op_sel_hi:[0,0] neg_lo:[1,1] neg_hi:[0,1]
	s_nop 0
	v_pk_fma_f32 v[48:49], v[22:23], v[32:33], v[42:43] op_sel_hi:[1,0,1]
	v_pk_add_f32 v[22:23], v[24:25], v[50:51]
	v_pk_add_f32 v[24:25], v[24:25], v[50:51] neg_lo:[0,1] neg_hi:[0,1]
	s_nop 0
	v_pk_mul_f32 v[42:43], v[24:25], v[38:39] op_sel:[1,0] op_sel_hi:[0,0] neg_lo:[1,1] neg_hi:[0,1]
	s_nop 0
	v_pk_fma_f32 v[52:53], v[24:25], v[34:35], v[42:43] op_sel_hi:[1,0,1]
	s_waitcnt lgkmcnt(5)
	v_pk_add_f32 v[24:25], v[26:27], v[54:55]
	v_pk_add_f32 v[26:27], v[26:27], v[54:55] neg_lo:[0,1] neg_hi:[0,1]
	s_nop 0
	v_pk_mul_f32 v[42:43], v[26:27], v[10:11] op_sel:[1,0] op_sel_hi:[0,0] neg_lo:[1,1] neg_hi:[0,1]
	s_nop 0
	v_pk_fma_f32 v[54:55], v[26:27], v[10:11], v[42:43] op_sel_hi:[1,0,1]
	v_pk_add_f32 v[26:27], v[28:29], v[56:57]
	v_pk_add_f32 v[28:29], v[28:29], v[56:57] neg_lo:[0,1] neg_hi:[0,1]
	s_nop 0
	v_pk_mul_f32 v[42:43], v[28:29], v[38:39] op_sel_hi:[1,0]
	s_nop 0
	v_pk_fma_f32 v[56:57], v[28:29], v[34:35], v[42:43] op_sel:[1,0,0] op_sel_hi:[0,0,1] neg_lo:[1,1,0] neg_hi:[0,1,0]
	s_waitcnt lgkmcnt(4)
	v_pk_add_f32 v[42:43], v[58:59], v[94:95] neg_lo:[0,1] neg_hi:[0,1]
	v_pk_add_f32 v[28:29], v[58:59], v[94:95]
	v_pk_mul_f32 v[50:51], v[42:43], v[36:37] op_sel_hi:[1,0]
	s_nop 0
	v_pk_fma_f32 v[58:59], v[42:43], v[32:33], v[50:51] op_sel:[1,0,0] op_sel_hi:[0,0,1] neg_lo:[1,1,0] neg_hi:[0,1,0]
	v_pk_add_f32 v[50:51], v[60:61], v[96:97] neg_lo:[0,1] neg_hi:[0,1]
	v_pk_add_f32 v[42:43], v[60:61], v[96:97]
	v_pk_mul_f32 v[60:61], v[50:51], v[46:47] op_sel_hi:[1,0]
	v_xor_b32_e32 v94, 0x80000000, v51
	v_mov_b32_e32 v95, v50
	s_waitcnt lgkmcnt(3)
	v_pk_add_f32 v[50:51], v[78:79], v[98:99]
	v_pk_add_f32 v[78:79], v[78:79], v[98:99] neg_lo:[0,1] neg_hi:[0,1]
	v_pk_fma_f32 v[60:61], v[94:95], v[30:31], v[60:61] op_sel_hi:[1,0,1] neg_lo:[0,1,0] neg_hi:[0,1,0]
	v_xor_b32_e32 v95, 0x80000000, v78
	v_mov_b32_e32 v94, v79
	v_pk_add_f32 v[78:79], v[80:81], v[100:101]
	v_pk_add_f32 v[80:81], v[80:81], v[100:101] neg_lo:[0,1] neg_hi:[0,1]
	s_nop 0
	v_pk_mul_f32 v[96:97], v[80:81], v[46:47] op_sel_hi:[1,0] neg_lo:[0,1] neg_hi:[0,1]
	s_nop 0
	v_pk_fma_f32 v[80:81], v[80:81], v[30:31], v[96:97] op_sel:[1,0,0] op_sel_hi:[0,0,1] neg_lo:[1,1,0] neg_hi:[0,1,0]
	s_waitcnt lgkmcnt(2)
	v_pk_add_f32 v[96:97], v[82:83], v[102:103]
	v_pk_add_f32 v[82:83], v[82:83], v[102:103] neg_lo:[0,1] neg_hi:[0,1]
	s_nop 0
	v_pk_mul_f32 v[98:99], v[82:83], v[36:37] op_sel_hi:[1,0] neg_lo:[0,1] neg_hi:[0,1]
	s_nop 0
	v_pk_fma_f32 v[82:83], v[82:83], v[32:33], v[98:99] op_sel:[1,0,0] op_sel_hi:[0,0,1] neg_lo:[1,1,0] neg_hi:[0,1,0]
	v_pk_add_f32 v[98:99], v[84:85], v[104:105]
	v_pk_add_f32 v[84:85], v[84:85], v[104:105] neg_lo:[0,1] neg_hi:[0,1]
	s_nop 0
	v_pk_mul_f32 v[100:101], v[84:85], v[38:39] op_sel_hi:[1,0] neg_lo:[0,1] neg_hi:[0,1]
	s_nop 0
	v_pk_fma_f32 v[84:85], v[84:85], v[34:35], v[100:101] op_sel:[1,0,0] op_sel_hi:[0,0,1] neg_lo:[1,1,0] neg_hi:[0,1,0]
	s_waitcnt lgkmcnt(1)
	v_pk_add_f32 v[100:101], v[86:87], v[106:107]
	v_pk_add_f32 v[86:87], v[86:87], v[106:107] neg_lo:[0,1] neg_hi:[0,1]
	s_nop 0
	v_pk_mul_f32 v[102:103], v[86:87], v[10:11] op_sel:[1,0] op_sel_hi:[0,0] neg_lo:[1,1] neg_hi:[0,1]
	s_nop 0
	v_pk_fma_f32 v[86:87], v[86:87], v[10:11], v[102:103] op_sel_hi:[1,0,1] neg_lo:[0,1,0] neg_hi:[0,1,0]
	v_pk_add_f32 v[102:103], v[88:89], v[108:109]
	v_pk_add_f32 v[88:89], v[88:89], v[108:109] neg_lo:[0,1] neg_hi:[0,1]
	s_nop 0
	v_pk_mul_f32 v[38:39], v[88:89], v[38:39] op_sel:[1,0] op_sel_hi:[0,0] neg_lo:[1,1] neg_hi:[0,1]
	s_nop 0
	v_pk_fma_f32 v[88:89], v[88:89], v[34:35], v[38:39] op_sel_hi:[1,0,1] neg_lo:[0,1,0] neg_hi:[0,1,0]
	s_waitcnt lgkmcnt(0)
	v_pk_add_f32 v[38:39], v[90:91], v[110:111] neg_lo:[0,1] neg_hi:[0,1]
	v_pk_add_f32 v[34:35], v[90:91], v[110:111]
	v_pk_mul_f32 v[90:91], v[38:39], v[36:37] op_sel:[1,0] op_sel_hi:[0,0] neg_lo:[1,1] neg_hi:[0,1]
	s_nop 0
	v_pk_fma_f32 v[90:91], v[38:39], v[32:33], v[90:91] op_sel_hi:[1,0,1] neg_lo:[0,1,0] neg_hi:[0,1,0]
	v_pk_add_f32 v[38:39], v[92:93], v[112:113]
	v_pk_add_f32 v[92:93], v[92:93], v[112:113] neg_lo:[0,1] neg_hi:[0,1]
	s_nop 0
	v_pk_mul_f32 v[46:47], v[92:93], v[46:47] op_sel:[1,0] op_sel_hi:[0,0] neg_lo:[1,1] neg_hi:[0,1]
	s_nop 0
	v_pk_fma_f32 v[92:93], v[92:93], v[30:31], v[46:47] op_sel_hi:[1,0,1] neg_lo:[0,1,0] neg_hi:[0,1,0]
	v_pk_add_f32 v[46:47], v[18:19], v[78:79]
	v_pk_add_f32 v[18:19], v[18:19], v[78:79] neg_lo:[0,1] neg_hi:[0,1]
	v_pk_add_f32 v[30:31], v[114:115], v[50:51]
	v_pk_mul_f32 v[78:79], v[18:19], v[36:37] op_sel:[1,0] op_sel_hi:[0,0] neg_lo:[1,1] neg_hi:[0,1]
	v_pk_add_f32 v[50:51], v[114:115], v[50:51] neg_lo:[0,1] neg_hi:[0,1]
	v_pk_fma_f32 v[78:79], v[18:19], v[32:33], v[78:79] op_sel_hi:[1,0,1]
	v_pk_add_f32 v[18:19], v[20:21], v[96:97]
	v_pk_add_f32 v[20:21], v[20:21], v[96:97] neg_lo:[0,1] neg_hi:[0,1]
	s_nop 0
	v_pk_mul_f32 v[96:97], v[20:21], v[10:11] op_sel:[1,0] op_sel_hi:[0,0] neg_lo:[1,1] neg_hi:[0,1]
	s_nop 0
	v_pk_fma_f32 v[20:21], v[20:21], v[10:11], v[96:97] op_sel_hi:[1,0,1]
	v_pk_add_f32 v[96:97], v[22:23], v[98:99]
	v_pk_add_f32 v[22:23], v[22:23], v[98:99] neg_lo:[0,1] neg_hi:[0,1]
	s_nop 0
	v_pk_mul_f32 v[98:99], v[22:23], v[36:37] op_sel_hi:[1,0]
	v_xor_b32_e32 v104, 0x80000000, v23
	v_mov_b32_e32 v105, v22
	v_pk_add_f32 v[22:23], v[24:25], v[100:101]
	v_pk_add_f32 v[24:25], v[24:25], v[100:101] neg_lo:[0,1] neg_hi:[0,1]
	v_pk_fma_f32 v[98:99], v[104:105], v[32:33], v[98:99] op_sel_hi:[1,0,1] neg_lo:[0,1,0] neg_hi:[0,1,0]
	v_xor_b32_e32 v101, 0x80000000, v24
	v_mov_b32_e32 v100, v25
	v_pk_add_f32 v[24:25], v[26:27], v[102:103]
	v_pk_add_f32 v[26:27], v[26:27], v[102:103] neg_lo:[0,1] neg_hi:[0,1]
	s_nop 0
	v_pk_mul_f32 v[102:103], v[26:27], v[36:37] op_sel_hi:[1,0] neg_lo:[0,1] neg_hi:[0,1]
	v_xor_b32_e32 v104, 0x80000000, v27
	v_mov_b32_e32 v105, v26
	v_pk_add_f32 v[26:27], v[28:29], v[34:35]
	v_pk_add_f32 v[28:29], v[28:29], v[34:35] neg_lo:[0,1] neg_hi:[0,1]
	v_pk_fma_f32 v[102:103], v[104:105], v[32:33], v[102:103] op_sel_hi:[1,0,1] neg_lo:[0,1,0] neg_hi:[0,1,0]
	v_pk_mul_f32 v[34:35], v[28:29], v[10:11] op_sel:[1,0] op_sel_hi:[0,0] neg_lo:[1,1] neg_hi:[0,1]
	v_pk_add_f32 v[104:105], v[30:31], v[22:23] neg_lo:[0,1] neg_hi:[0,1]
	v_pk_fma_f32 v[28:29], v[28:29], v[10:11], v[34:35] op_sel_hi:[1,0,1] neg_lo:[0,1,0] neg_hi:[0,1,0]
	v_pk_add_f32 v[34:35], v[42:43], v[38:39]
	v_pk_add_f32 v[38:39], v[42:43], v[38:39] neg_lo:[0,1] neg_hi:[0,1]
	s_nop 0
	v_pk_mul_f32 v[42:43], v[38:39], v[36:37] op_sel:[1,0] op_sel_hi:[0,0] neg_lo:[1,1] neg_hi:[0,1]
	s_nop 0
	v_pk_fma_f32 v[42:43], v[38:39], v[32:33], v[42:43] op_sel_hi:[1,0,1] neg_lo:[0,1,0] neg_hi:[0,1,0]
	v_pk_add_f32 v[38:39], v[30:31], v[22:23]
	v_pk_add_f32 v[22:23], v[46:47], v[24:25]
	v_pk_add_f32 v[24:25], v[46:47], v[24:25] neg_lo:[0,1] neg_hi:[0,1]
	s_nop 0
	v_pk_mul_f32 v[30:31], v[24:25], v[10:11] op_sel:[1,0] op_sel_hi:[0,0] neg_lo:[1,1] neg_hi:[0,1]
	s_nop 0
	v_pk_fma_f32 v[24:25], v[24:25], v[10:11], v[30:31] op_sel_hi:[1,0,1]
	v_pk_add_f32 v[30:31], v[18:19], v[26:27]
	v_pk_add_f32 v[18:19], v[18:19], v[26:27] neg_lo:[0,1] neg_hi:[0,1]
	s_nop 0
	v_xor_b32_e32 v27, 0x80000000, v18
	v_mov_b32_e32 v26, v19
	v_pk_add_f32 v[18:19], v[96:97], v[34:35]
	v_pk_add_f32 v[34:35], v[96:97], v[34:35] neg_lo:[0,1] neg_hi:[0,1]
	s_nop 0
	v_pk_mul_f32 v[46:47], v[34:35], v[10:11] op_sel:[1,0] op_sel_hi:[0,0] neg_lo:[1,1] neg_hi:[0,1]
	s_nop 0
	v_pk_fma_f32 v[34:35], v[34:35], v[10:11], v[46:47] op_sel_hi:[1,0,1] neg_lo:[0,1,0] neg_hi:[0,1,0]
	v_pk_add_f32 v[46:47], v[38:39], v[30:31]
	v_pk_add_f32 v[38:39], v[38:39], v[30:31] neg_lo:[0,1] neg_hi:[0,1]
	v_pk_add_f32 v[30:31], v[22:23], v[18:19]
	v_pk_add_f32 v[18:19], v[22:23], v[18:19] neg_lo:[0,1] neg_hi:[0,1]
	v_pk_add_f32 v[96:97], v[46:47], v[30:31]
	v_xor_b32_e32 v23, 0x80000000, v18
	v_mov_b32_e32 v22, v19
	v_pk_add_f32 v[18:19], v[104:105], v[26:27]
	v_pk_add_f32 v[104:105], v[104:105], v[26:27] neg_lo:[0,1] neg_hi:[0,1]
	v_pk_add_f32 v[26:27], v[24:25], v[34:35]
	v_pk_add_f32 v[24:25], v[24:25], v[34:35] neg_lo:[0,1] neg_hi:[0,1]
	v_pk_add_f32 v[30:31], v[46:47], v[30:31] neg_lo:[0,1] neg_hi:[0,1]
	v_xor_b32_e32 v35, 0x80000000, v24
	v_mov_b32_e32 v34, v25
	v_pk_add_f32 v[24:25], v[50:51], v[100:101]
	v_pk_add_f32 v[100:101], v[50:51], v[100:101] neg_lo:[0,1] neg_hi:[0,1]
	v_pk_add_f32 v[50:51], v[78:79], v[102:103] neg_lo:[0,1] neg_hi:[0,1]
	v_pk_add_f32 v[46:47], v[38:39], v[22:23]
	v_pk_add_f32 v[22:23], v[38:39], v[22:23] neg_lo:[0,1] neg_hi:[0,1]
	v_pk_add_f32 v[106:107], v[18:19], v[26:27]
	v_pk_add_f32 v[26:27], v[18:19], v[26:27] neg_lo:[0,1] neg_hi:[0,1]
	v_pk_add_f32 v[38:39], v[104:105], v[34:35]
	v_pk_add_f32 v[18:19], v[104:105], v[34:35] neg_lo:[0,1] neg_hi:[0,1]
	v_pk_add_f32 v[34:35], v[78:79], v[102:103]
	v_pk_mul_f32 v[78:79], v[10:11], v[50:51] op_sel:[0,1] op_sel_hi:[0,0] neg_lo:[1,1] neg_hi:[1,0]
	v_pk_fma_f32 v[78:79], v[10:11], v[50:51], v[78:79] op_sel_hi:[0,1,1]
	v_pk_add_f32 v[50:51], v[20:21], v[28:29]
	v_pk_add_f32 v[20:21], v[20:21], v[28:29] neg_lo:[0,1] neg_hi:[0,1]
	s_nop 0
	v_xor_b32_e32 v29, 0x80000000, v20
	v_mov_b32_e32 v28, v21
	v_pk_add_f32 v[20:21], v[98:99], v[42:43]
	v_pk_add_f32 v[42:43], v[98:99], v[42:43] neg_lo:[0,1] neg_hi:[0,1]
	s_nop 0
	v_pk_mul_f32 v[98:99], v[10:11], v[42:43] op_sel:[0,1] op_sel_hi:[0,0] neg_lo:[1,1] neg_hi:[1,0]
	v_pk_fma_f32 v[42:43], v[10:11], v[42:43], v[98:99] op_sel_hi:[0,1,1] neg_lo:[1,0,0] neg_hi:[1,0,0]
	v_pk_add_f32 v[98:99], v[24:25], v[50:51]
	v_pk_add_f32 v[24:25], v[24:25], v[50:51] neg_lo:[0,1] neg_hi:[0,1]
	v_pk_add_f32 v[50:51], v[34:35], v[20:21]
	v_pk_add_f32 v[20:21], v[34:35], v[20:21] neg_lo:[0,1] neg_hi:[0,1]
	v_pk_add_f32 v[104:105], v[98:99], v[50:51]
	v_xor_b32_e32 v103, 0x80000000, v20
	v_mov_b32_e32 v102, v21
	v_pk_add_f32 v[34:35], v[98:99], v[50:51] neg_lo:[0,1] neg_hi:[0,1]
	v_pk_add_f32 v[20:21], v[100:101], v[28:29]
	v_pk_add_f32 v[98:99], v[100:101], v[28:29] neg_lo:[0,1] neg_hi:[0,1]
	v_pk_add_f32 v[28:29], v[78:79], v[42:43]
	v_pk_add_f32 v[42:43], v[78:79], v[42:43] neg_lo:[0,1] neg_hi:[0,1]
	v_pk_add_f32 v[100:101], v[20:21], v[28:29]
	v_xor_b32_e32 v79, 0x80000000, v42
	v_mov_b32_e32 v78, v43
	v_pk_add_f32 v[28:29], v[20:21], v[28:29] neg_lo:[0,1] neg_hi:[0,1]
	v_pk_add_f32 v[42:43], v[98:99], v[78:79]
	v_pk_add_f32 v[20:21], v[98:99], v[78:79] neg_lo:[0,1] neg_hi:[0,1]
	v_pk_add_f32 v[78:79], v[40:41], v[94:95]
	v_pk_add_f32 v[94:95], v[40:41], v[94:95] neg_lo:[0,1] neg_hi:[0,1]
	v_pk_add_f32 v[40:41], v[44:45], v[80:81]
	v_pk_add_f32 v[44:45], v[44:45], v[80:81] neg_lo:[0,1] neg_hi:[0,1]
	v_pk_add_f32 v[50:51], v[24:25], v[102:103]
	v_pk_mul_f32 v[80:81], v[36:37], v[44:45] op_sel:[0,1] op_sel_hi:[0,0] neg_lo:[1,1] neg_hi:[1,0]
	v_pk_fma_f32 v[44:45], v[32:33], v[44:45], v[80:81] op_sel_hi:[0,1,1]
	v_pk_add_f32 v[80:81], v[48:49], v[82:83]
	v_pk_add_f32 v[48:49], v[48:49], v[82:83] neg_lo:[0,1] neg_hi:[0,1]
	v_pk_add_f32 v[24:25], v[24:25], v[102:103] neg_lo:[0,1] neg_hi:[0,1]
	v_pk_mul_f32 v[82:83], v[10:11], v[48:49] op_sel:[0,1] op_sel_hi:[0,0] neg_lo:[1,1] neg_hi:[1,0]
	v_pk_fma_f32 v[82:83], v[10:11], v[48:49], v[82:83] op_sel_hi:[0,1,1]
	v_pk_add_f32 v[48:49], v[52:53], v[84:85]
	v_pk_add_f32 v[52:53], v[52:53], v[84:85] neg_lo:[0,1] neg_hi:[0,1]
	s_nop 0
	v_pk_mul_f32 v[84:85], v[32:33], v[52:53] op_sel:[0,1] op_sel_hi:[0,0] neg_lo:[1,1] neg_hi:[1,0]
	v_pk_fma_f32 v[52:53], v[36:37], v[52:53], v[84:85] op_sel_hi:[0,1,1]
	v_pk_add_f32 v[84:85], v[54:55], v[86:87]
	v_pk_add_f32 v[54:55], v[54:55], v[86:87] neg_lo:[0,1] neg_hi:[0,1]
	s_nop 0
	v_xor_b32_e32 v87, 0x80000000, v54
	v_mov_b32_e32 v86, v55
	v_pk_add_f32 v[54:55], v[56:57], v[88:89]
	v_pk_add_f32 v[56:57], v[56:57], v[88:89] neg_lo:[0,1] neg_hi:[0,1]
	s_nop 0
	v_pk_mul_f32 v[88:89], v[32:33], v[56:57] op_sel:[0,1] op_sel_hi:[0,0] neg_lo:[1,1] neg_hi:[1,0]
	v_pk_fma_f32 v[56:57], v[36:37], v[56:57], v[88:89] op_sel_hi:[0,1,1] neg_lo:[1,0,0] neg_hi:[1,0,0]
	v_pk_add_f32 v[88:89], v[58:59], v[90:91]
	v_pk_add_f32 v[58:59], v[58:59], v[90:91] neg_lo:[0,1] neg_hi:[0,1]
	s_nop 0
	v_pk_mul_f32 v[90:91], v[10:11], v[58:59] op_sel:[0,1] op_sel_hi:[0,0] neg_lo:[1,1] neg_hi:[1,0]
	v_pk_fma_f32 v[58:59], v[10:11], v[58:59], v[90:91] op_sel_hi:[0,1,1] neg_lo:[1,0,0] neg_hi:[1,0,0]
	v_pk_add_f32 v[90:91], v[60:61], v[92:93]
	v_pk_add_f32 v[60:61], v[60:61], v[92:93] neg_lo:[0,1] neg_hi:[0,1]
	s_nop 0
	v_pk_mul_f32 v[36:37], v[36:37], v[60:61] op_sel:[0,1] op_sel_hi:[0,0] neg_lo:[1,1] neg_hi:[1,0]
	v_pk_fma_f32 v[36:37], v[32:33], v[60:61], v[36:37] op_sel_hi:[0,1,1] neg_lo:[1,0,0] neg_hi:[1,0,0]
	v_pk_add_f32 v[32:33], v[78:79], v[84:85]
	v_pk_add_f32 v[60:61], v[78:79], v[84:85] neg_lo:[0,1] neg_hi:[0,1]
	v_pk_add_f32 v[78:79], v[54:55], v[40:41]
	v_pk_add_f32 v[40:41], v[40:41], v[54:55] neg_lo:[0,1] neg_hi:[0,1]
	s_nop 0
	v_pk_mul_f32 v[54:55], v[10:11], v[40:41] op_sel:[0,1] op_sel_hi:[0,0] neg_lo:[1,1] neg_hi:[1,0]
	v_pk_fma_f32 v[54:55], v[10:11], v[40:41], v[54:55] op_sel_hi:[0,1,1]
	v_pk_add_f32 v[40:41], v[80:81], v[88:89]
	v_pk_add_f32 v[80:81], v[80:81], v[88:89] neg_lo:[0,1] neg_hi:[0,1]
	s_nop 0
	v_xor_b32_e32 v85, 0x80000000, v80
	v_mov_b32_e32 v84, v81
	v_pk_add_f32 v[80:81], v[48:49], v[90:91]
	v_pk_add_f32 v[48:49], v[48:49], v[90:91] neg_lo:[0,1] neg_hi:[0,1]
	v_pk_add_f32 v[90:91], v[78:79], v[80:81]
	v_pk_mul_f32 v[88:89], v[10:11], v[48:49] op_sel:[0,1] op_sel_hi:[0,0] neg_lo:[1,1] neg_hi:[1,0]
	v_pk_fma_f32 v[48:49], v[10:11], v[48:49], v[88:89] op_sel_hi:[0,1,1] neg_lo:[1,0,0] neg_hi:[1,0,0]
	v_pk_add_f32 v[88:89], v[32:33], v[40:41]
	v_pk_add_f32 v[32:33], v[32:33], v[40:41] neg_lo:[0,1] neg_hi:[0,1]
	v_pk_add_f32 v[40:41], v[78:79], v[80:81] neg_lo:[0,1] neg_hi:[0,1]
	v_pk_add_f32 v[80:81], v[88:89], v[90:91] neg_lo:[0,1] neg_hi:[0,1]
	v_pk_add_f32 v[92:93], v[32:33], v[40:41] op_sel:[0,1] op_sel_hi:[1,0] neg_hi:[0,1]
	v_pk_add_f32 v[40:41], v[32:33], v[40:41] op_sel:[0,1] op_sel_hi:[1,0] neg_lo:[0,1]
	v_pk_add_f32 v[78:79], v[54:55], v[48:49]
	v_pk_add_f32 v[48:49], v[54:55], v[48:49] neg_lo:[0,1] neg_hi:[0,1]
	v_pk_add_f32 v[32:33], v[60:61], v[84:85]
	v_pk_add_f32 v[60:61], v[60:61], v[84:85] neg_lo:[0,1] neg_hi:[0,1]
	v_xor_b32_e32 v55, 0x80000000, v48
	v_mov_b32_e32 v54, v49
	v_pk_add_f32 v[84:85], v[32:33], v[78:79]
	v_pk_add_f32 v[48:49], v[32:33], v[78:79] neg_lo:[0,1] neg_hi:[0,1]
	v_pk_add_f32 v[78:79], v[60:61], v[54:55]
	v_pk_add_f32 v[32:33], v[60:61], v[54:55] neg_lo:[0,1] neg_hi:[0,1]
	v_pk_add_f32 v[54:55], v[94:95], v[86:87]
	v_pk_add_f32 v[60:61], v[94:95], v[86:87] neg_lo:[0,1] neg_hi:[0,1]
	v_pk_add_f32 v[86:87], v[56:57], v[44:45]
	v_pk_add_f32 v[44:45], v[44:45], v[56:57] neg_lo:[0,1] neg_hi:[0,1]
	v_pk_add_f32 v[88:89], v[88:89], v[90:91]
	v_pk_mul_f32 v[56:57], v[10:11], v[44:45] op_sel:[0,1] op_sel_hi:[0,0] neg_lo:[1,1] neg_hi:[1,0]
	v_pk_fma_f32 v[56:57], v[10:11], v[44:45], v[56:57] op_sel_hi:[0,1,1]
	v_pk_add_f32 v[44:45], v[82:83], v[58:59]
	v_pk_add_f32 v[58:59], v[82:83], v[58:59] neg_lo:[0,1] neg_hi:[0,1]
	s_nop 0
	v_xor_b32_e32 v83, 0x80000000, v58
	v_mov_b32_e32 v82, v59
	v_pk_add_f32 v[58:59], v[52:53], v[36:37]
	v_pk_add_f32 v[36:37], v[52:53], v[36:37] neg_lo:[0,1] neg_hi:[0,1]
	s_nop 0
	v_pk_mul_f32 v[52:53], v[10:11], v[36:37] op_sel:[0,1] op_sel_hi:[0,0] neg_lo:[1,1] neg_hi:[1,0]
	v_pk_fma_f32 v[36:37], v[10:11], v[36:37], v[52:53] op_sel_hi:[0,1,1] neg_lo:[1,0,0] neg_hi:[1,0,0]
	v_pk_add_f32 v[52:53], v[54:55], v[44:45]
	v_pk_add_f32 v[44:45], v[54:55], v[44:45] neg_lo:[0,1] neg_hi:[0,1]
	v_pk_add_f32 v[54:55], v[86:87], v[58:59]
	v_pk_add_f32 v[58:59], v[86:87], v[58:59] neg_lo:[0,1] neg_hi:[0,1]
	s_nop 0
	v_xor_b32_e32 v87, 0x80000000, v58
	v_mov_b32_e32 v86, v59
	v_pk_add_f32 v[58:59], v[52:53], v[54:55]
	v_pk_add_f32 v[54:55], v[52:53], v[54:55] neg_lo:[0,1] neg_hi:[0,1]
	v_pk_add_f32 v[52:53], v[60:61], v[82:83]
	v_pk_add_f32 v[60:61], v[60:61], v[82:83] neg_lo:[0,1] neg_hi:[0,1]
	v_pk_add_f32 v[82:83], v[56:57], v[36:37]
	v_pk_add_f32 v[36:37], v[56:57], v[36:37] neg_lo:[0,1] neg_hi:[0,1]
	v_pk_add_f32 v[94:95], v[44:45], v[86:87]
	v_pk_add_f32 v[44:45], v[44:45], v[86:87] neg_lo:[0,1] neg_hi:[0,1]
	v_pk_add_f32 v[86:87], v[52:53], v[82:83]
	v_pk_add_f32 v[52:53], v[52:53], v[82:83] neg_lo:[0,1] neg_hi:[0,1]
	v_pk_add_f32 v[82:83], v[60:61], v[36:37] op_sel:[0,1] op_sel_hi:[1,0] neg_hi:[0,1]
	v_pk_add_f32 v[36:37], v[60:61], v[36:37] op_sel:[0,1] op_sel_hi:[1,0] neg_lo:[0,1]
	v_pk_fma_f32 v[60:61], v[14:15], s[92:93], v[14:15] op_sel:[1,0,0] op_sel_hi:[0,1,1]
	v_pk_mul_f32 v[56:57], v[96:97], s[14:15] op_sel:[1,0] neg_lo:[1,0]
	v_pk_mul_f32 v[90:91], v[60:61], v[88:89] op_sel:[1,1] op_sel_hi:[0,1] neg_lo:[0,1]
	v_pk_fma_f32 v[56:57], v[96:97], s[42:43], v[56:57] op_sel_hi:[0,1,1]
	v_pk_fma_f32 v[88:89], v[60:61], v[88:89], v[90:91] op_sel_hi:[1,0,1]
	ds_write2_b64 v76, v[56:57], v[88:89] offset1:16
	v_pk_mul_f32 v[56:57], v[14:15], v[60:61] op_sel:[1,1] op_sel_hi:[0,1] neg_lo:[0,1]
	v_pk_fma_f32 v[56:57], v[14:15], v[60:61], v[56:57] op_sel_hi:[1,0,1]
	s_nop 0
	v_pk_mul_f32 v[60:61], v[56:57], v[104:105] op_sel:[1,1] op_sel_hi:[0,1] neg_lo:[0,1]
	v_pk_mul_f32 v[76:77], v[14:15], v[56:57] op_sel:[1,1] op_sel_hi:[0,1] neg_lo:[0,1]
	v_pk_fma_f32 v[60:61], v[56:57], v[104:105], v[60:61] op_sel_hi:[1,0,1]
	v_pk_fma_f32 v[56:57], v[14:15], v[56:57], v[76:77] op_sel_hi:[1,0,1]
	s_nop 0
	v_pk_mul_f32 v[76:77], v[56:57], v[58:59] op_sel:[1,1] op_sel_hi:[0,1] neg_lo:[0,1]
	v_pk_fma_f32 v[58:59], v[56:57], v[58:59], v[76:77] op_sel_hi:[1,0,1]
	ds_write2_b64 v75, v[60:61], v[58:59] offset0:32 offset1:48
	v_pk_mul_f32 v[58:59], v[14:15], v[56:57] op_sel:[1,1] op_sel_hi:[0,1] neg_lo:[0,1]
	v_pk_fma_f32 v[56:57], v[14:15], v[56:57], v[58:59] op_sel_hi:[1,0,1]
	s_nop 0
	v_pk_mul_f32 v[58:59], v[56:57], v[106:107] op_sel:[1,1] op_sel_hi:[0,1] neg_lo:[0,1]
	v_pk_mul_f32 v[60:61], v[14:15], v[56:57] op_sel:[1,1] op_sel_hi:[0,1] neg_lo:[0,1]
	v_pk_fma_f32 v[58:59], v[56:57], v[106:107], v[58:59] op_sel_hi:[1,0,1]
	v_pk_fma_f32 v[56:57], v[14:15], v[56:57], v[60:61] op_sel_hi:[1,0,1]
	s_nop 0
	v_pk_mul_f32 v[60:61], v[56:57], v[84:85] op_sel:[1,1] op_sel_hi:[0,1] neg_lo:[0,1]
	v_pk_fma_f32 v[60:61], v[56:57], v[84:85], v[60:61] op_sel_hi:[1,0,1]
	ds_write2_b64 v74, v[58:59], v[60:61] offset0:64 offset1:80
	v_pk_mul_f32 v[58:59], v[14:15], v[56:57] op_sel:[1,1] op_sel_hi:[0,1] neg_lo:[0,1]
	v_pk_fma_f32 v[56:57], v[14:15], v[56:57], v[58:59] op_sel_hi:[1,0,1]
	s_nop 0
	v_pk_mul_f32 v[58:59], v[56:57], v[100:101] op_sel:[1,1] op_sel_hi:[0,1] neg_lo:[0,1]
	v_pk_mul_f32 v[60:61], v[14:15], v[56:57] op_sel:[1,1] op_sel_hi:[0,1] neg_lo:[0,1]
	v_pk_fma_f32 v[58:59], v[56:57], v[100:101], v[58:59] op_sel_hi:[1,0,1]
	v_pk_fma_f32 v[56:57], v[14:15], v[56:57], v[60:61] op_sel_hi:[1,0,1]
	s_nop 0
	v_pk_mul_f32 v[60:61], v[56:57], v[86:87] op_sel:[1,1] op_sel_hi:[0,1] neg_lo:[0,1]
	v_pk_fma_f32 v[60:61], v[56:57], v[86:87], v[60:61] op_sel_hi:[1,0,1]
	ds_write2_b64 v73, v[58:59], v[60:61] offset0:96 offset1:112
	v_pk_mul_f32 v[58:59], v[14:15], v[56:57] op_sel:[1,1] op_sel_hi:[0,1] neg_lo:[0,1]
	v_pk_fma_f32 v[56:57], v[14:15], v[56:57], v[58:59] op_sel_hi:[1,0,1]
	s_nop 0
	v_pk_mul_f32 v[58:59], v[56:57], v[46:47] op_sel:[1,1] op_sel_hi:[0,1] neg_lo:[0,1]
	v_pk_fma_f32 v[46:47], v[56:57], v[46:47], v[58:59] op_sel_hi:[1,0,1]
	v_pk_mul_f32 v[58:59], v[14:15], v[56:57] op_sel:[1,1] op_sel_hi:[0,1] neg_lo:[0,1]
	v_pk_fma_f32 v[56:57], v[14:15], v[56:57], v[58:59] op_sel_hi:[1,0,1]
	s_nop 0
	v_pk_mul_f32 v[58:59], v[56:57], v[92:93] op_sel:[1,1] op_sel_hi:[0,1] neg_lo:[0,1]
	v_pk_fma_f32 v[58:59], v[56:57], v[92:93], v[58:59] op_sel_hi:[1,0,1]
	ds_write2_b64 v72, v[46:47], v[58:59] offset0:128 offset1:144
	v_pk_mul_f32 v[46:47], v[14:15], v[56:57] op_sel:[1,1] op_sel_hi:[0,1] neg_lo:[0,1]
	v_pk_fma_f32 v[46:47], v[14:15], v[56:57], v[46:47] op_sel_hi:[1,0,1]
	s_nop 0
	v_pk_mul_f32 v[56:57], v[46:47], v[50:51] op_sel:[1,1] op_sel_hi:[0,1] neg_lo:[0,1]
	v_pk_fma_f32 v[50:51], v[46:47], v[50:51], v[56:57] op_sel_hi:[1,0,1]
	v_pk_mul_f32 v[56:57], v[14:15], v[46:47] op_sel:[1,1] op_sel_hi:[0,1] neg_lo:[0,1]
	v_pk_fma_f32 v[46:47], v[14:15], v[46:47], v[56:57] op_sel_hi:[1,0,1]
	s_nop 0
	v_pk_mul_f32 v[56:57], v[46:47], v[94:95] op_sel:[1,1] op_sel_hi:[0,1] neg_lo:[0,1]
	v_pk_fma_f32 v[56:57], v[46:47], v[94:95], v[56:57] op_sel_hi:[1,0,1]
	ds_write2_b64 v71, v[50:51], v[56:57] offset0:160 offset1:176
	v_pk_mul_f32 v[50:51], v[14:15], v[46:47] op_sel:[1,1] op_sel_hi:[0,1] neg_lo:[0,1]
	v_pk_fma_f32 v[46:47], v[14:15], v[46:47], v[50:51] op_sel_hi:[1,0,1]
	s_nop 0
	v_pk_mul_f32 v[50:51], v[38:39], v[46:47] op_sel:[1,1] op_sel_hi:[1,0] neg_lo:[1,0]
	s_nop 0
	v_pk_fma_f32 v[38:39], v[38:39], v[46:47], v[50:51] op_sel_hi:[0,1,1]
	v_pk_mul_f32 v[50:51], v[14:15], v[46:47] op_sel:[1,1] op_sel_hi:[0,1] neg_lo:[0,1]
	v_pk_fma_f32 v[46:47], v[14:15], v[46:47], v[50:51] op_sel_hi:[1,0,1]
	s_nop 0
	v_pk_mul_f32 v[50:51], v[46:47], v[78:79] op_sel:[1,1] op_sel_hi:[0,1] neg_lo:[0,1]
	v_pk_fma_f32 v[50:51], v[46:47], v[78:79], v[50:51] op_sel_hi:[1,0,1]
	ds_write2_b64 v70, v[38:39], v[50:51] offset0:192 offset1:208
	v_pk_mul_f32 v[38:39], v[14:15], v[46:47] op_sel:[1,1] op_sel_hi:[0,1] neg_lo:[0,1]
	v_pk_fma_f32 v[38:39], v[14:15], v[46:47], v[38:39] op_sel_hi:[1,0,1]
	s_nop 0
	v_pk_mul_f32 v[46:47], v[42:43], v[38:39] op_sel:[1,1] op_sel_hi:[1,0] neg_lo:[1,0]
	s_nop 0
	v_pk_fma_f32 v[42:43], v[42:43], v[38:39], v[46:47] op_sel_hi:[0,1,1]
	v_pk_mul_f32 v[46:47], v[14:15], v[38:39] op_sel:[1,1] op_sel_hi:[0,1] neg_lo:[0,1]
	v_pk_fma_f32 v[38:39], v[14:15], v[38:39], v[46:47] op_sel_hi:[1,0,1]
	s_nop 0
	v_pk_mul_f32 v[46:47], v[38:39], v[82:83] op_sel:[1,1] op_sel_hi:[0,1] neg_lo:[0,1]
	v_pk_fma_f32 v[46:47], v[38:39], v[82:83], v[46:47] op_sel_hi:[1,0,1]
	ds_write2_b64 v69, v[42:43], v[46:47] offset0:224 offset1:240
	v_pk_mul_f32 v[42:43], v[14:15], v[38:39] op_sel:[1,1] op_sel_hi:[0,1] neg_lo:[0,1]
	v_pk_fma_f32 v[38:39], v[14:15], v[38:39], v[42:43] op_sel_hi:[1,0,1]
	s_nop 0
	v_pk_mul_f32 v[42:43], v[30:31], v[38:39] op_sel:[1,1] op_sel_hi:[1,0] neg_lo:[1,0]
	s_nop 0
	v_pk_fma_f32 v[30:31], v[30:31], v[38:39], v[42:43] op_sel_hi:[0,1,1]
	v_pk_mul_f32 v[42:43], v[14:15], v[38:39] op_sel:[1,1] op_sel_hi:[0,1] neg_lo:[0,1]
	v_pk_fma_f32 v[38:39], v[14:15], v[38:39], v[42:43] op_sel_hi:[1,0,1]
	s_nop 0
	v_pk_mul_f32 v[42:43], v[80:81], v[38:39] op_sel:[1,1] op_sel_hi:[1,0] neg_lo:[1,0]
	s_nop 0
	v_pk_fma_f32 v[42:43], v[80:81], v[38:39], v[42:43] op_sel_hi:[0,1,1]
	ds_write2_b64 v68, v[30:31], v[42:43] offset1:16
	v_pk_mul_f32 v[30:31], v[14:15], v[38:39] op_sel:[1,1] op_sel_hi:[0,1] neg_lo:[0,1]
	v_pk_fma_f32 v[30:31], v[14:15], v[38:39], v[30:31] op_sel_hi:[1,0,1]
	s_nop 0
	v_pk_mul_f32 v[38:39], v[34:35], v[30:31] op_sel:[1,1] op_sel_hi:[1,0] neg_lo:[1,0]
	s_nop 0
	v_pk_fma_f32 v[34:35], v[34:35], v[30:31], v[38:39] op_sel_hi:[0,1,1]
	v_pk_mul_f32 v[38:39], v[14:15], v[30:31] op_sel:[1,1] op_sel_hi:[0,1] neg_lo:[0,1]
	v_pk_fma_f32 v[30:31], v[14:15], v[30:31], v[38:39] op_sel_hi:[1,0,1]
	s_nop 0
	v_pk_mul_f32 v[38:39], v[54:55], v[30:31] op_sel:[1,1] op_sel_hi:[1,0] neg_lo:[1,0]
	s_nop 0
	v_pk_fma_f32 v[38:39], v[54:55], v[30:31], v[38:39] op_sel_hi:[0,1,1]
	ds_write2_b64 v67, v[34:35], v[38:39] offset0:32 offset1:48
	v_pk_mul_f32 v[34:35], v[14:15], v[30:31] op_sel:[1,1] op_sel_hi:[0,1] neg_lo:[0,1]
	v_pk_fma_f32 v[30:31], v[14:15], v[30:31], v[34:35] op_sel_hi:[1,0,1]
	s_nop 0
	v_pk_mul_f32 v[34:35], v[26:27], v[30:31] op_sel:[1,1] op_sel_hi:[1,0] neg_lo:[1,0]
	s_nop 0
	v_pk_fma_f32 v[26:27], v[26:27], v[30:31], v[34:35] op_sel_hi:[0,1,1]
	v_pk_mul_f32 v[34:35], v[14:15], v[30:31] op_sel:[1,1] op_sel_hi:[0,1] neg_lo:[0,1]
	v_pk_fma_f32 v[30:31], v[14:15], v[30:31], v[34:35] op_sel_hi:[1,0,1]
	s_nop 0
	v_pk_mul_f32 v[34:35], v[48:49], v[30:31] op_sel:[1,1] op_sel_hi:[1,0] neg_lo:[1,0]
	s_nop 0
	v_pk_fma_f32 v[34:35], v[48:49], v[30:31], v[34:35] op_sel_hi:[0,1,1]
	ds_write2_b64 v66, v[26:27], v[34:35] offset0:64 offset1:80
	v_pk_mul_f32 v[26:27], v[14:15], v[30:31] op_sel:[1,1] op_sel_hi:[0,1] neg_lo:[0,1]
	v_pk_fma_f32 v[26:27], v[14:15], v[30:31], v[26:27] op_sel_hi:[1,0,1]
	s_nop 0
	v_pk_mul_f32 v[30:31], v[28:29], v[26:27] op_sel:[1,1] op_sel_hi:[1,0] neg_lo:[1,0]
	s_nop 0
	v_pk_fma_f32 v[28:29], v[28:29], v[26:27], v[30:31] op_sel_hi:[0,1,1]
	v_pk_mul_f32 v[30:31], v[14:15], v[26:27] op_sel:[1,1] op_sel_hi:[0,1] neg_lo:[0,1]
	v_pk_fma_f32 v[26:27], v[14:15], v[26:27], v[30:31] op_sel_hi:[1,0,1]
	s_nop 0
	v_pk_mul_f32 v[30:31], v[52:53], v[26:27] op_sel:[1,1] op_sel_hi:[1,0] neg_lo:[1,0]
	s_nop 0
	v_pk_fma_f32 v[30:31], v[52:53], v[26:27], v[30:31] op_sel_hi:[0,1,1]
	ds_write2_b64 v65, v[28:29], v[30:31] offset0:96 offset1:112
	v_pk_mul_f32 v[28:29], v[14:15], v[26:27] op_sel:[1,1] op_sel_hi:[0,1] neg_lo:[0,1]
	v_pk_fma_f32 v[26:27], v[14:15], v[26:27], v[28:29] op_sel_hi:[1,0,1]
	s_nop 0
	v_pk_mul_f32 v[28:29], v[22:23], v[26:27] op_sel:[1,1] op_sel_hi:[1,0] neg_lo:[1,0]
	s_nop 0
	v_pk_fma_f32 v[22:23], v[22:23], v[26:27], v[28:29] op_sel_hi:[0,1,1]
	v_pk_mul_f32 v[28:29], v[14:15], v[26:27] op_sel:[1,1] op_sel_hi:[0,1] neg_lo:[0,1]
	v_pk_fma_f32 v[26:27], v[14:15], v[26:27], v[28:29] op_sel_hi:[1,0,1]
	s_nop 0
	v_pk_mul_f32 v[28:29], v[40:41], v[26:27] op_sel:[1,1] op_sel_hi:[1,0] neg_lo:[1,0]
	s_nop 0
	v_pk_fma_f32 v[28:29], v[40:41], v[26:27], v[28:29] op_sel_hi:[0,1,1]
	ds_write2_b64 v64, v[22:23], v[28:29] offset0:128 offset1:144
	v_pk_mul_f32 v[22:23], v[14:15], v[26:27] op_sel:[1,1] op_sel_hi:[0,1] neg_lo:[0,1]
	v_pk_fma_f32 v[22:23], v[14:15], v[26:27], v[22:23] op_sel_hi:[1,0,1]
	s_nop 0
	v_pk_mul_f32 v[26:27], v[24:25], v[22:23] op_sel:[1,1] op_sel_hi:[1,0] neg_lo:[1,0]
	s_nop 0
	v_pk_fma_f32 v[24:25], v[24:25], v[22:23], v[26:27] op_sel_hi:[0,1,1]
	v_pk_mul_f32 v[26:27], v[14:15], v[22:23] op_sel:[1,1] op_sel_hi:[0,1] neg_lo:[0,1]
	v_pk_fma_f32 v[22:23], v[14:15], v[22:23], v[26:27] op_sel_hi:[1,0,1]
	s_nop 0
	v_pk_mul_f32 v[26:27], v[44:45], v[22:23] op_sel:[1,1] op_sel_hi:[1,0] neg_lo:[1,0]
	s_nop 0
	v_pk_fma_f32 v[26:27], v[44:45], v[22:23], v[26:27] op_sel_hi:[0,1,1]
	ds_write2_b64 v63, v[24:25], v[26:27] offset0:160 offset1:176
	v_pk_mul_f32 v[24:25], v[14:15], v[22:23] op_sel:[1,1] op_sel_hi:[0,1] neg_lo:[0,1]
	v_pk_fma_f32 v[22:23], v[14:15], v[22:23], v[24:25] op_sel_hi:[1,0,1]
	s_nop 0
	v_pk_mul_f32 v[24:25], v[18:19], v[22:23] op_sel:[1,1] op_sel_hi:[1,0] neg_lo:[1,0]
	s_nop 0
	v_pk_fma_f32 v[18:19], v[18:19], v[22:23], v[24:25] op_sel_hi:[0,1,1]
	v_pk_mul_f32 v[24:25], v[14:15], v[22:23] op_sel:[1,1] op_sel_hi:[0,1] neg_lo:[0,1]
	v_pk_fma_f32 v[22:23], v[14:15], v[22:23], v[24:25] op_sel_hi:[1,0,1]
	s_nop 0
	v_pk_mul_f32 v[24:25], v[32:33], v[22:23] op_sel:[1,1] op_sel_hi:[1,0] neg_lo:[1,0]
	s_nop 0
	v_pk_fma_f32 v[24:25], v[32:33], v[22:23], v[24:25] op_sel_hi:[0,1,1]
	ds_write2_b64 v62, v[18:19], v[24:25] offset0:192 offset1:208
	v_pk_mul_f32 v[18:19], v[14:15], v[22:23] op_sel:[1,1] op_sel_hi:[0,1] neg_lo:[0,1]
	v_pk_fma_f32 v[18:19], v[14:15], v[22:23], v[18:19] op_sel_hi:[1,0,1]
	s_nop 0
	v_pk_mul_f32 v[22:23], v[20:21], v[18:19] op_sel:[1,1] op_sel_hi:[1,0] neg_lo:[1,0]
	s_nop 0
	v_pk_fma_f32 v[20:21], v[20:21], v[18:19], v[22:23] op_sel_hi:[0,1,1]
	v_pk_mul_f32 v[22:23], v[14:15], v[18:19] op_sel:[1,1] op_sel_hi:[0,1] neg_lo:[0,1]
	v_pk_fma_f32 v[14:15], v[14:15], v[18:19], v[22:23] op_sel_hi:[1,0,1]
	s_nop 0
	v_pk_mul_f32 v[18:19], v[36:37], v[14:15] op_sel:[1,1] op_sel_hi:[1,0] neg_lo:[1,0]
	s_nop 0
	v_pk_fma_f32 v[14:15], v[36:37], v[14:15], v[18:19] op_sel_hi:[0,1,1]
	ds_write2_b64 v13, v[20:21], v[14:15] offset0:224 offset1:240
	v_mov_b32_e32 v14, v1
	v_mov_b32_e32 v10, v178
	v_mov_b32_e32 v13, v177
	s_waitcnt lgkmcnt(0)
	s_barrier
	v_mov_b32_e32 v50, v168
	v_xor_b32_e32 v18, 1, v13
	v_lshlrev_b32_e32 v10, 3, v10
	v_lshlrev_b32_e32 v18, 3, v18
	v_add3_u32 v20, 0, v18, v10
	v_xor_b32_e32 v18, 2, v13
	v_lshlrev_b32_e32 v18, 3, v18
	v_xor_b32_e32 v26, 5, v13
	v_add3_u32 v22, 0, v18, v10
	v_xor_b32_e32 v18, 3, v13
	v_lshlrev_b32_e32 v26, 3, v26
	v_lshlrev_b32_e32 v15, 3, v13
	v_lshlrev_b32_e32 v18, 3, v18
	v_add3_u32 v28, 0, v26, v10
	v_xor_b32_e32 v26, 6, v13
	v_add3_u32 v15, 0, v15, v10
	v_add3_u32 v24, 0, v18, v10
	v_lshlrev_b32_e32 v26, 3, v26
	v_xor_b32_e32 v34, 9, v13
	ds_read_b64 v[18:19], v15
	ds_read_b64 v[20:21], v20
	ds_read_b64 v[22:23], v22
	ds_read_b64 v[24:25], v24
	v_xor_b32_e32 v15, 4, v13
	v_add3_u32 v30, 0, v26, v10
	v_xor_b32_e32 v26, 7, v13
	v_lshlrev_b32_e32 v34, 3, v34
	v_lshlrev_b32_e32 v15, 3, v15
	v_lshlrev_b32_e32 v26, 3, v26
	v_add3_u32 v36, 0, v34, v10
	v_xor_b32_e32 v34, 10, v13
	v_add3_u32 v15, 0, v15, v10
	v_add3_u32 v32, 0, v26, v10
	v_lshlrev_b32_e32 v34, 3, v34
	ds_read_b64 v[26:27], v15
	ds_read_b64 v[28:29], v28
	ds_read_b64 v[30:31], v30
	ds_read_b64 v[32:33], v32
	v_xor_b32_e32 v15, 8, v13
	v_add3_u32 v38, 0, v34, v10
	v_xor_b32_e32 v34, 11, v13
	v_lshlrev_b32_e32 v15, 3, v15
	v_lshlrev_b32_e32 v34, 3, v34
	v_xor_b32_e32 v42, 13, v13
	v_add3_u32 v15, 0, v15, v10
	v_add3_u32 v40, 0, v34, v10
	v_lshlrev_b32_e32 v42, 3, v42
	ds_read_b64 v[34:35], v15
	ds_read_b64 v[36:37], v36
	ds_read_b64 v[38:39], v38
	ds_read_b64 v[40:41], v40
	v_xor_b32_e32 v15, 12, v13
	v_add3_u32 v44, 0, v42, v10
	v_xor_b32_e32 v42, 14, v13
	v_xor_b32_e32 v13, 15, v13
	v_lshlrev_b32_e32 v15, 3, v15
	v_lshlrev_b32_e32 v42, 3, v42
	v_lshlrev_b32_e32 v13, 3, v13
	v_add3_u32 v15, 0, v15, v10
	v_add3_u32 v46, 0, v42, v10
	v_add3_u32 v10, 0, v13, v10
	ds_read_b64 v[42:43], v15
	ds_read_b64 v[44:45], v44
	ds_read_b64 v[46:47], v46
	ds_read_b64 v[48:49], v10
	v_mov_b32_e32 v10, v164
	v_mov_b32_e32 v13, v167
	v_mov_b32_e32 v10, v165
	s_waitcnt lgkmcnt(7)
	v_pk_add_f32 v[54:55], v[18:19], v[34:35]
	v_mov_b32_e32 v10, v166
	v_pk_add_f32 v[18:19], v[18:19], v[34:35] neg_lo:[0,1] neg_hi:[0,1]
	s_waitcnt lgkmcnt(6)
	v_pk_add_f32 v[34:35], v[20:21], v[36:37]
	v_pk_add_f32 v[20:21], v[20:21], v[36:37] neg_lo:[0,1] neg_hi:[0,1]
	v_mov_b32_e32 v13, v169
	v_mov_b32_e32 v52, v170
	v_ashrrev_i32_e32 v15, 31, v14
	v_pk_mul_f32 v[36:37], v[20:21], v[52:53] op_sel:[1,0] op_sel_hi:[0,0] neg_lo:[1,1] neg_hi:[0,1]
	v_mov_b32_e32 v13, v171
	v_pk_fma_f32 v[20:21], v[20:21], v[10:11], v[36:37] op_sel_hi:[1,0,1]
	s_waitcnt lgkmcnt(5)
	v_pk_add_f32 v[36:37], v[22:23], v[38:39]
	v_pk_add_f32 v[22:23], v[22:23], v[38:39] neg_lo:[0,1] neg_hi:[0,1]
	s_movk_i32 s85, 0x1000
	v_pk_mul_f32 v[38:39], v[22:23], v[50:51] op_sel:[1,0] op_sel_hi:[0,0] neg_lo:[1,1] neg_hi:[0,1]
	v_mov_b32_e32 v13, v172
	v_pk_fma_f32 v[22:23], v[22:23], v[50:51], v[38:39] op_sel_hi:[1,0,1]
	s_waitcnt lgkmcnt(4)
	v_pk_add_f32 v[38:39], v[24:25], v[40:41]
	v_pk_add_f32 v[24:25], v[24:25], v[40:41] neg_lo:[0,1] neg_hi:[0,1]
	s_movk_i32 s84, 0x2000
	v_pk_mul_f32 v[40:41], v[24:25], v[52:53] op_sel_hi:[1,0]
	s_nop 0
	v_pk_fma_f32 v[24:25], v[24:25], v[10:11], v[40:41] op_sel:[1,0,0] op_sel_hi:[0,0,1] neg_lo:[1,1,0] neg_hi:[0,1,0]
	s_waitcnt lgkmcnt(3)
	v_pk_add_f32 v[40:41], v[26:27], v[42:43]
	v_pk_add_f32 v[26:27], v[26:27], v[42:43] neg_lo:[0,1] neg_hi:[0,1]
	v_mov_b32_e32 v13, v177
	v_xor_b32_e32 v43, 0x80000000, v26
	v_mov_b32_e32 v42, v27
	s_waitcnt lgkmcnt(2)
	v_pk_add_f32 v[26:27], v[28:29], v[44:45]
	v_pk_add_f32 v[28:29], v[28:29], v[44:45] neg_lo:[0,1] neg_hi:[0,1]
	s_movk_i32 s88, 0x6000
	v_pk_mul_f32 v[44:45], v[28:29], v[52:53] op_sel_hi:[1,0] neg_lo:[0,1] neg_hi:[0,1]
	s_nop 0
	v_pk_fma_f32 v[28:29], v[28:29], v[10:11], v[44:45] op_sel:[1,0,0] op_sel_hi:[0,0,1] neg_lo:[1,1,0] neg_hi:[0,1,0]
	s_waitcnt lgkmcnt(1)
	v_pk_add_f32 v[44:45], v[30:31], v[46:47]
	v_pk_add_f32 v[30:31], v[30:31], v[46:47] neg_lo:[0,1] neg_hi:[0,1]
	s_mov_b32 s0, 0x8000
	v_pk_mul_f32 v[46:47], v[30:31], v[50:51] op_sel:[1,0] op_sel_hi:[0,0] neg_lo:[1,1] neg_hi:[0,1]
	s_movk_i32 s86, 0x5000
	v_pk_fma_f32 v[30:31], v[30:31], v[50:51], v[46:47] op_sel_hi:[1,0,1] neg_lo:[0,1,0] neg_hi:[0,1,0]
	s_waitcnt lgkmcnt(0)
	v_pk_add_f32 v[46:47], v[32:33], v[48:49]
	v_pk_add_f32 v[32:33], v[32:33], v[48:49] neg_lo:[0,1] neg_hi:[0,1]
	v_mov_b32_e32 v72, v165
	v_pk_mul_f32 v[48:49], v[32:33], v[52:53] op_sel:[1,0] op_sel_hi:[0,0] neg_lo:[1,1] neg_hi:[0,1]
	v_pk_add_f32 v[52:53], v[34:35], v[26:27]
	v_pk_add_f32 v[26:27], v[34:35], v[26:27] neg_lo:[0,1] neg_hi:[0,1]
	v_pk_fma_f32 v[32:33], v[32:33], v[10:11], v[48:49] op_sel_hi:[1,0,1] neg_lo:[0,1,0] neg_hi:[0,1,0]
	v_pk_mul_f32 v[34:35], v[26:27], v[50:51] op_sel:[1,0] op_sel_hi:[0,0] neg_lo:[1,1] neg_hi:[0,1]
	v_pk_add_f32 v[48:49], v[54:55], v[40:41]
	v_pk_fma_f32 v[26:27], v[26:27], v[50:51], v[34:35] op_sel_hi:[1,0,1]
	v_pk_add_f32 v[34:35], v[36:37], v[44:45]
	v_pk_add_f32 v[36:37], v[36:37], v[44:45] neg_lo:[0,1] neg_hi:[0,1]
	v_pk_add_f32 v[40:41], v[54:55], v[40:41] neg_lo:[0,1] neg_hi:[0,1]
	v_xor_b32_e32 v45, 0x80000000, v36
	v_mov_b32_e32 v44, v37
	v_pk_add_f32 v[36:37], v[38:39], v[46:47]
	v_pk_add_f32 v[38:39], v[38:39], v[46:47] neg_lo:[0,1] neg_hi:[0,1]
	v_mov_b32_e32 v10, v179
	v_pk_mul_f32 v[46:47], v[38:39], v[50:51] op_sel:[1,0] op_sel_hi:[0,0] neg_lo:[1,1] neg_hi:[0,1]
	v_mov_b32_e32 v74, v167
	v_pk_fma_f32 v[38:39], v[38:39], v[50:51], v[46:47] op_sel_hi:[1,0,1] neg_lo:[0,1,0] neg_hi:[0,1,0]
	v_pk_add_f32 v[46:47], v[48:49], v[34:35]
	v_pk_add_f32 v[34:35], v[48:49], v[34:35] neg_lo:[0,1] neg_hi:[0,1]
	v_pk_add_f32 v[48:49], v[52:53], v[36:37]
	v_pk_add_f32 v[36:37], v[52:53], v[36:37] neg_lo:[0,1] neg_hi:[0,1]
	v_mov_b32_e32 v76, v169
	v_xor_b32_e32 v53, 0x80000000, v36
	v_mov_b32_e32 v52, v37
	v_pk_add_f32 v[36:37], v[46:47], v[48:49]
	v_pk_add_f32 v[46:47], v[46:47], v[48:49] neg_lo:[0,1] neg_hi:[0,1]
	v_pk_add_f32 v[48:49], v[34:35], v[52:53]
	v_pk_add_f32 v[34:35], v[34:35], v[52:53] neg_lo:[0,1] neg_hi:[0,1]
	v_pk_add_f32 v[52:53], v[40:41], v[44:45]
	v_pk_add_f32 v[40:41], v[40:41], v[44:45] neg_lo:[0,1] neg_hi:[0,1]
	v_pk_add_f32 v[44:45], v[26:27], v[38:39]
	v_pk_add_f32 v[26:27], v[26:27], v[38:39] neg_lo:[0,1] neg_hi:[0,1]
	v_mov_b32_e32 v78, v171
	v_xor_b32_e32 v39, 0x80000000, v26
	v_mov_b32_e32 v38, v27
	v_pk_add_f32 v[26:27], v[52:53], v[44:45]
	v_pk_add_f32 v[44:45], v[52:53], v[44:45] neg_lo:[0,1] neg_hi:[0,1]
	v_pk_add_f32 v[52:53], v[40:41], v[38:39]
	v_pk_add_f32 v[38:39], v[40:41], v[38:39] neg_lo:[0,1] neg_hi:[0,1]
	v_pk_add_f32 v[40:41], v[18:19], v[42:43]
	v_pk_add_f32 v[18:19], v[18:19], v[42:43] neg_lo:[0,1] neg_hi:[0,1]
	v_pk_add_f32 v[42:43], v[20:21], v[28:29]
	v_pk_add_f32 v[20:21], v[20:21], v[28:29] neg_lo:[0,1] neg_hi:[0,1]
	v_mov_b32_e32 v83, v11
	v_pk_mul_f32 v[28:29], v[50:51], v[20:21] op_sel:[0,1] op_sel_hi:[0,0] neg_lo:[1,1] neg_hi:[1,0]
	v_pk_fma_f32 v[20:21], v[50:51], v[20:21], v[28:29] op_sel_hi:[0,1,1]
	v_pk_add_f32 v[28:29], v[22:23], v[30:31]
	v_pk_add_f32 v[22:23], v[22:23], v[30:31] neg_lo:[0,1] neg_hi:[0,1]
	s_mov_b32 s1, 0xe000
	v_xor_b32_e32 v31, 0x80000000, v22
	v_mov_b32_e32 v30, v23
	v_pk_add_f32 v[22:23], v[24:25], v[32:33]
	v_pk_add_f32 v[24:25], v[24:25], v[32:33] neg_lo:[0,1] neg_hi:[0,1]
	s_mov_b32 s8, 0x8000
	v_pk_mul_f32 v[32:33], v[50:51], v[24:25] op_sel:[0,1] op_sel_hi:[0,0] neg_lo:[1,1] neg_hi:[1,0]
	v_pk_fma_f32 v[24:25], v[50:51], v[24:25], v[32:33] op_sel_hi:[0,1,1] neg_lo:[1,0,0] neg_hi:[1,0,0]
	v_pk_add_f32 v[32:33], v[40:41], v[28:29]
	v_pk_add_f32 v[28:29], v[40:41], v[28:29] neg_lo:[0,1] neg_hi:[0,1]
	v_pk_add_f32 v[40:41], v[42:43], v[22:23]
	v_pk_add_f32 v[22:23], v[42:43], v[22:23] neg_lo:[0,1] neg_hi:[0,1]
	v_mov_b32_e32 v50, v168
	v_xor_b32_e32 v43, 0x80000000, v22
	v_mov_b32_e32 v42, v23
	v_pk_add_f32 v[22:23], v[32:33], v[40:41]
	v_pk_add_f32 v[32:33], v[32:33], v[40:41] neg_lo:[0,1] neg_hi:[0,1]
	v_pk_add_f32 v[40:41], v[28:29], v[42:43]
	v_pk_add_f32 v[28:29], v[28:29], v[42:43] neg_lo:[0,1] neg_hi:[0,1]
	v_pk_add_f32 v[42:43], v[18:19], v[30:31]
	v_pk_add_f32 v[18:19], v[18:19], v[30:31] neg_lo:[0,1] neg_hi:[0,1]
	v_pk_add_f32 v[30:31], v[20:21], v[24:25]
	v_pk_add_f32 v[20:21], v[20:21], v[24:25] neg_lo:[0,1] neg_hi:[0,1]
	s_mov_b32 s7, 0xa000
	v_xor_b32_e32 v25, 0x80000000, v20
	v_mov_b32_e32 v24, v21
	v_pk_add_f32 v[20:21], v[42:43], v[30:31]
	v_pk_add_f32 v[30:31], v[42:43], v[30:31] neg_lo:[0,1] neg_hi:[0,1]
	v_pk_add_f32 v[42:43], v[18:19], v[24:25]
	v_pk_add_f32 v[18:19], v[18:19], v[24:25] neg_lo:[0,1] neg_hi:[0,1]
	v_lshl_add_u64 v[24:25], v[14:15], 3, s[48:49]
	global_store_dwordx2 v[24:25], v[36:37], off
	v_add_u32_e32 v24, 0x200, v14
	v_ashrrev_i32_e32 v25, 31, v24
	v_lshl_add_u64 v[24:25], v[24:25], 3, s[48:49]
	global_store_dwordx2 v[24:25], v[22:23], off
	v_add_u32_e32 v22, 0x400, v14
	v_ashrrev_i32_e32 v23, 31, v22
	v_lshl_add_u64 v[22:23], v[22:23], 3, s[48:49]
	global_store_dwordx2 v[22:23], v[26:27], off
	v_add_u32_e32 v22, 0x600, v14
	v_ashrrev_i32_e32 v23, 31, v22
	v_lshl_add_u64 v[22:23], v[22:23], 3, s[48:49]
	global_store_dwordx2 v[22:23], v[20:21], off
	v_add_u32_e32 v20, 0x800, v14
	v_ashrrev_i32_e32 v21, 31, v20
	v_lshl_add_u64 v[20:21], v[20:21], 3, s[48:49]
	global_store_dwordx2 v[20:21], v[48:49], off
	v_add_u32_e32 v20, 0xa00, v14
	v_ashrrev_i32_e32 v21, 31, v20
	v_lshl_add_u64 v[20:21], v[20:21], 3, s[48:49]
	global_store_dwordx2 v[20:21], v[40:41], off
	v_add_u32_e32 v20, 0xc00, v14
	v_ashrrev_i32_e32 v21, 31, v20
	v_lshl_add_u64 v[20:21], v[20:21], 3, s[48:49]
	global_store_dwordx2 v[20:21], v[52:53], off
	v_add_u32_e32 v20, 0xe00, v14
	v_ashrrev_i32_e32 v21, 31, v20
	v_lshl_add_u64 v[20:21], v[20:21], 3, s[48:49]
	global_store_dwordx2 v[20:21], v[42:43], off
	v_add_u32_e32 v20, 0x1000, v14
	v_ashrrev_i32_e32 v21, 31, v20
	v_lshl_add_u64 v[20:21], v[20:21], 3, s[48:49]
	global_store_dwordx2 v[20:21], v[46:47], off
	v_add_u32_e32 v20, 0x1200, v14
	v_ashrrev_i32_e32 v21, 31, v20
	v_lshl_add_u64 v[20:21], v[20:21], 3, s[48:49]
	global_store_dwordx2 v[20:21], v[32:33], off
	v_add_u32_e32 v20, 0x1400, v14
	v_ashrrev_i32_e32 v21, 31, v20
	v_lshl_add_u64 v[20:21], v[20:21], 3, s[48:49]
	global_store_dwordx2 v[20:21], v[44:45], off
	v_add_u32_e32 v20, 0x1600, v14
	v_ashrrev_i32_e32 v21, 31, v20
	v_lshl_add_u64 v[20:21], v[20:21], 3, s[48:49]
	global_store_dwordx2 v[20:21], v[30:31], off
	v_add_u32_e32 v20, 0x1800, v14
	v_ashrrev_i32_e32 v21, 31, v20
	v_lshl_add_u64 v[20:21], v[20:21], 3, s[48:49]
	global_store_dwordx2 v[20:21], v[34:35], off
	v_add_u32_e32 v20, 0x1a00, v14
	v_ashrrev_i32_e32 v21, 31, v20
	v_lshl_add_u64 v[20:21], v[20:21], 3, s[48:49]
	global_store_dwordx2 v[20:21], v[28:29], off
	v_add_u32_e32 v20, 0x1c00, v14
	v_ashrrev_i32_e32 v21, 31, v20
	v_lshl_add_u64 v[20:21], v[20:21], 3, s[48:49]
	global_store_dwordx2 v[20:21], v[38:39], off
	v_add_u32_e32 v20, 0x1e00, v14
	v_ashrrev_i32_e32 v21, 31, v20
	v_lshl_add_u64 v[20:21], v[20:21], 3, s[48:49]
	global_store_dwordx2 v[20:21], v[18:19], off
	v_mov_b32_e32 v52, v170
	v_xor_b32_e32 v18, 1, v13
	v_lshlrev_b32_e32 v10, 3, v10
	v_lshlrev_b32_e32 v18, 3, v18
	v_add3_u32 v20, 0, v18, v10
	v_xor_b32_e32 v18, 2, v13
	v_lshlrev_b32_e32 v18, 3, v18
	v_xor_b32_e32 v26, 5, v13
	v_add3_u32 v22, 0, v18, v10
	v_xor_b32_e32 v18, 3, v13
	v_lshlrev_b32_e32 v26, 3, v26
	v_lshlrev_b32_e32 v15, 3, v13
	v_lshlrev_b32_e32 v18, 3, v18
	v_add3_u32 v28, 0, v26, v10
	v_xor_b32_e32 v26, 6, v13
	v_add3_u32 v15, 0, v15, v10
	v_add3_u32 v24, 0, v18, v10
	v_lshlrev_b32_e32 v26, 3, v26
	v_xor_b32_e32 v34, 9, v13
	ds_read_b64 v[18:19], v15
	ds_read_b64 v[20:21], v20
	ds_read_b64 v[22:23], v22
	ds_read_b64 v[24:25], v24
	v_xor_b32_e32 v15, 4, v13
	v_add3_u32 v30, 0, v26, v10
	v_xor_b32_e32 v26, 7, v13
	v_lshlrev_b32_e32 v34, 3, v34
	v_lshlrev_b32_e32 v15, 3, v15
	v_lshlrev_b32_e32 v26, 3, v26
	v_add3_u32 v36, 0, v34, v10
	v_xor_b32_e32 v34, 10, v13
	v_add3_u32 v15, 0, v15, v10
	v_add3_u32 v32, 0, v26, v10
	v_lshlrev_b32_e32 v34, 3, v34
	ds_read_b64 v[26:27], v15
	ds_read_b64 v[28:29], v28
	ds_read_b64 v[30:31], v30
	ds_read_b64 v[32:33], v32
	v_xor_b32_e32 v15, 8, v13
	v_add3_u32 v38, 0, v34, v10
	v_xor_b32_e32 v34, 11, v13
	v_lshlrev_b32_e32 v15, 3, v15
	v_lshlrev_b32_e32 v34, 3, v34
	v_xor_b32_e32 v42, 13, v13
	v_add3_u32 v15, 0, v15, v10
	v_add3_u32 v40, 0, v34, v10
	v_lshlrev_b32_e32 v42, 3, v42
	ds_read_b64 v[34:35], v15
	ds_read_b64 v[36:37], v36
	ds_read_b64 v[38:39], v38
	ds_read_b64 v[40:41], v40
	v_xor_b32_e32 v15, 12, v13
	v_add3_u32 v44, 0, v42, v10
	v_xor_b32_e32 v42, 14, v13
	v_xor_b32_e32 v13, 15, v13
	v_lshlrev_b32_e32 v15, 3, v15
	v_lshlrev_b32_e32 v42, 3, v42
	v_lshlrev_b32_e32 v13, 3, v13
	v_add3_u32 v15, 0, v15, v10
	v_add3_u32 v46, 0, v42, v10
	v_add3_u32 v10, 0, v13, v10
	ds_read_b64 v[42:43], v15
	ds_read_b64 v[44:45], v44
	ds_read_b64 v[46:47], v46
	ds_read_b64 v[48:49], v10
	v_mov_b32_e32 v10, v164
	v_mov_b32_e32 v13, v167
	v_mov_b32_e32 v10, v165
	s_waitcnt lgkmcnt(7)
	v_pk_add_f32 v[54:55], v[18:19], v[34:35]
	v_mov_b32_e32 v10, v166
	v_pk_add_f32 v[18:19], v[18:19], v[34:35] neg_lo:[0,1] neg_hi:[0,1]
	s_waitcnt lgkmcnt(6)
	v_pk_add_f32 v[34:35], v[20:21], v[36:37]
	v_pk_add_f32 v[20:21], v[20:21], v[36:37] neg_lo:[0,1] neg_hi:[0,1]
	v_mov_b32_e32 v13, v169
	s_mov_b32 s9, 0x9000
	v_pk_mul_f32 v[36:37], v[20:21], v[52:53] op_sel:[1,0] op_sel_hi:[0,0] neg_lo:[1,1] neg_hi:[0,1]
	v_mov_b32_e32 v13, v171
	v_pk_fma_f32 v[20:21], v[20:21], v[10:11], v[36:37] op_sel_hi:[1,0,1]
	s_waitcnt lgkmcnt(5)
	v_pk_add_f32 v[36:37], v[22:23], v[38:39]
	v_pk_add_f32 v[22:23], v[22:23], v[38:39] neg_lo:[0,1] neg_hi:[0,1]
	s_mov_b32 s5, 0xb000
	v_pk_mul_f32 v[38:39], v[22:23], v[50:51] op_sel:[1,0] op_sel_hi:[0,0] neg_lo:[1,1] neg_hi:[0,1]
	v_mov_b32_e32 v13, v172
	v_pk_fma_f32 v[22:23], v[22:23], v[50:51], v[38:39] op_sel_hi:[1,0,1]
	s_waitcnt lgkmcnt(4)
	v_pk_add_f32 v[38:39], v[24:25], v[40:41]
	v_pk_add_f32 v[24:25], v[24:25], v[40:41] neg_lo:[0,1] neg_hi:[0,1]
	s_mov_b32 s6, 0xc000
	v_pk_mul_f32 v[40:41], v[24:25], v[52:53] op_sel_hi:[1,0]
	s_nop 0
	v_pk_fma_f32 v[24:25], v[24:25], v[10:11], v[40:41] op_sel:[1,0,0] op_sel_hi:[0,0,1] neg_lo:[1,1,0] neg_hi:[0,1,0]
	s_waitcnt lgkmcnt(3)
	v_pk_add_f32 v[40:41], v[26:27], v[42:43]
	v_pk_add_f32 v[26:27], v[26:27], v[42:43] neg_lo:[0,1] neg_hi:[0,1]
	s_mov_b32 s4, 0xd000
	v_xor_b32_e32 v43, 0x80000000, v26
	v_mov_b32_e32 v42, v27
	s_waitcnt lgkmcnt(2)
	v_pk_add_f32 v[26:27], v[28:29], v[44:45]
	v_pk_add_f32 v[28:29], v[28:29], v[44:45] neg_lo:[0,1] neg_hi:[0,1]
	s_nop 0
	v_pk_mul_f32 v[44:45], v[28:29], v[52:53] op_sel_hi:[1,0] neg_lo:[0,1] neg_hi:[0,1]
	s_nop 0
	v_pk_fma_f32 v[28:29], v[28:29], v[10:11], v[44:45] op_sel:[1,0,0] op_sel_hi:[0,0,1] neg_lo:[1,1,0] neg_hi:[0,1,0]
	s_waitcnt lgkmcnt(1)
	v_pk_add_f32 v[44:45], v[30:31], v[46:47]
	v_pk_add_f32 v[30:31], v[30:31], v[46:47] neg_lo:[0,1] neg_hi:[0,1]
	s_nop 0
	v_pk_mul_f32 v[46:47], v[30:31], v[50:51] op_sel:[1,0] op_sel_hi:[0,0] neg_lo:[1,1] neg_hi:[0,1]
	s_nop 0
	v_pk_fma_f32 v[30:31], v[30:31], v[50:51], v[46:47] op_sel_hi:[1,0,1] neg_lo:[0,1,0] neg_hi:[0,1,0]
	s_waitcnt lgkmcnt(0)
	v_pk_add_f32 v[46:47], v[32:33], v[48:49]
	v_pk_add_f32 v[32:33], v[32:33], v[48:49] neg_lo:[0,1] neg_hi:[0,1]
	s_nop 0
	v_pk_mul_f32 v[48:49], v[32:33], v[52:53] op_sel:[1,0] op_sel_hi:[0,0] neg_lo:[1,1] neg_hi:[0,1]
	v_pk_add_f32 v[52:53], v[34:35], v[26:27]
	v_pk_add_f32 v[26:27], v[34:35], v[26:27] neg_lo:[0,1] neg_hi:[0,1]
	v_pk_fma_f32 v[32:33], v[32:33], v[10:11], v[48:49] op_sel_hi:[1,0,1] neg_lo:[0,1,0] neg_hi:[0,1,0]
	v_pk_mul_f32 v[34:35], v[26:27], v[50:51] op_sel:[1,0] op_sel_hi:[0,0] neg_lo:[1,1] neg_hi:[0,1]
	v_pk_add_f32 v[48:49], v[54:55], v[40:41]
	v_pk_fma_f32 v[26:27], v[26:27], v[50:51], v[34:35] op_sel_hi:[1,0,1]
	v_pk_add_f32 v[34:35], v[36:37], v[44:45]
	v_pk_add_f32 v[36:37], v[36:37], v[44:45] neg_lo:[0,1] neg_hi:[0,1]
	v_pk_add_f32 v[40:41], v[54:55], v[40:41] neg_lo:[0,1] neg_hi:[0,1]
	v_xor_b32_e32 v45, 0x80000000, v36
	v_mov_b32_e32 v44, v37
	v_pk_add_f32 v[36:37], v[38:39], v[46:47]
	v_pk_add_f32 v[38:39], v[38:39], v[46:47] neg_lo:[0,1] neg_hi:[0,1]
	v_mov_b32_e32 v10, v164
	v_pk_mul_f32 v[46:47], v[38:39], v[50:51] op_sel:[1,0] op_sel_hi:[0,0] neg_lo:[1,1] neg_hi:[0,1]
	s_nop 0
	v_pk_fma_f32 v[38:39], v[38:39], v[50:51], v[46:47] op_sel_hi:[1,0,1] neg_lo:[0,1,0] neg_hi:[0,1,0]
	v_pk_add_f32 v[46:47], v[48:49], v[34:35]
	v_pk_add_f32 v[34:35], v[48:49], v[34:35] neg_lo:[0,1] neg_hi:[0,1]
	v_pk_add_f32 v[48:49], v[52:53], v[36:37]
	v_pk_add_f32 v[36:37], v[52:53], v[36:37] neg_lo:[0,1] neg_hi:[0,1]
	s_nop 0
	v_xor_b32_e32 v53, 0x80000000, v36
	v_mov_b32_e32 v52, v37
	v_pk_add_f32 v[36:37], v[46:47], v[48:49]
	v_pk_add_f32 v[46:47], v[46:47], v[48:49] neg_lo:[0,1] neg_hi:[0,1]
	v_pk_add_f32 v[48:49], v[34:35], v[52:53]
	v_pk_add_f32 v[34:35], v[34:35], v[52:53] neg_lo:[0,1] neg_hi:[0,1]
	v_pk_add_f32 v[52:53], v[40:41], v[44:45]
	v_pk_add_f32 v[40:41], v[40:41], v[44:45] neg_lo:[0,1] neg_hi:[0,1]
	v_pk_add_f32 v[44:45], v[26:27], v[38:39]
	v_pk_add_f32 v[26:27], v[26:27], v[38:39] neg_lo:[0,1] neg_hi:[0,1]
	s_nop 0
	v_xor_b32_e32 v39, 0x80000000, v26
	v_mov_b32_e32 v38, v27
	v_pk_add_f32 v[26:27], v[52:53], v[44:45]
	v_pk_add_f32 v[44:45], v[52:53], v[44:45] neg_lo:[0,1] neg_hi:[0,1]
	v_pk_add_f32 v[52:53], v[40:41], v[38:39]
	v_pk_add_f32 v[38:39], v[40:41], v[38:39] neg_lo:[0,1] neg_hi:[0,1]
	v_pk_add_f32 v[40:41], v[18:19], v[42:43]
	v_pk_add_f32 v[18:19], v[18:19], v[42:43] neg_lo:[0,1] neg_hi:[0,1]
	v_pk_add_f32 v[42:43], v[20:21], v[28:29]
	v_pk_add_f32 v[20:21], v[20:21], v[28:29] neg_lo:[0,1] neg_hi:[0,1]
	s_nop 0
	v_pk_mul_f32 v[28:29], v[50:51], v[20:21] op_sel:[0,1] op_sel_hi:[0,0] neg_lo:[1,1] neg_hi:[1,0]
	v_pk_fma_f32 v[20:21], v[50:51], v[20:21], v[28:29] op_sel_hi:[0,1,1]
	v_pk_add_f32 v[28:29], v[22:23], v[30:31]
	v_pk_add_f32 v[22:23], v[22:23], v[30:31] neg_lo:[0,1] neg_hi:[0,1]
	s_nop 0
	v_xor_b32_e32 v31, 0x80000000, v22
	v_mov_b32_e32 v30, v23
	v_pk_add_f32 v[22:23], v[24:25], v[32:33]
	v_pk_add_f32 v[24:25], v[24:25], v[32:33] neg_lo:[0,1] neg_hi:[0,1]
	s_nop 0
	v_pk_mul_f32 v[32:33], v[50:51], v[24:25] op_sel:[0,1] op_sel_hi:[0,0] neg_lo:[1,1] neg_hi:[1,0]
	v_pk_fma_f32 v[24:25], v[50:51], v[24:25], v[32:33] op_sel_hi:[0,1,1] neg_lo:[1,0,0] neg_hi:[1,0,0]
	v_pk_add_f32 v[32:33], v[40:41], v[28:29]
	v_pk_add_f32 v[28:29], v[40:41], v[28:29] neg_lo:[0,1] neg_hi:[0,1]
	v_pk_add_f32 v[40:41], v[42:43], v[22:23]
	v_pk_add_f32 v[22:23], v[42:43], v[22:23] neg_lo:[0,1] neg_hi:[0,1]
	s_nop 0
	v_xor_b32_e32 v43, 0x80000000, v22
	v_mov_b32_e32 v42, v23
	v_pk_add_f32 v[22:23], v[32:33], v[40:41]
	v_pk_add_f32 v[32:33], v[32:33], v[40:41] neg_lo:[0,1] neg_hi:[0,1]
	v_pk_add_f32 v[40:41], v[28:29], v[42:43]
	v_pk_add_f32 v[28:29], v[28:29], v[42:43] neg_lo:[0,1] neg_hi:[0,1]
	v_pk_add_f32 v[42:43], v[18:19], v[30:31]
	v_pk_add_f32 v[18:19], v[18:19], v[30:31] neg_lo:[0,1] neg_hi:[0,1]
	v_pk_add_f32 v[30:31], v[20:21], v[24:25]
	v_pk_add_f32 v[20:21], v[20:21], v[24:25] neg_lo:[0,1] neg_hi:[0,1]
	s_nop 0
	v_xor_b32_e32 v25, 0x80000000, v20
	v_mov_b32_e32 v24, v21
	v_pk_add_f32 v[20:21], v[42:43], v[30:31]
	v_pk_add_f32 v[30:31], v[42:43], v[30:31] neg_lo:[0,1] neg_hi:[0,1]
	v_pk_add_f32 v[42:43], v[18:19], v[24:25]
	v_pk_add_f32 v[18:19], v[18:19], v[24:25] neg_lo:[0,1] neg_hi:[0,1]
	v_add_u32_e32 v24, 0x2000, v14
	v_ashrrev_i32_e32 v25, 31, v24
	v_lshl_add_u64 v[24:25], v[24:25], 3, s[48:49]
	global_store_dwordx2 v[24:25], v[36:37], off
	v_add_u32_e32 v24, 0x2200, v14
	v_ashrrev_i32_e32 v25, 31, v24
	v_lshl_add_u64 v[24:25], v[24:25], 3, s[48:49]
	global_store_dwordx2 v[24:25], v[22:23], off
	v_add_u32_e32 v22, 0x2400, v14
	v_ashrrev_i32_e32 v23, 31, v22
	v_lshl_add_u64 v[22:23], v[22:23], 3, s[48:49]
	global_store_dwordx2 v[22:23], v[26:27], off
	v_add_u32_e32 v22, 0x2600, v14
	v_ashrrev_i32_e32 v23, 31, v22
	v_lshl_add_u64 v[22:23], v[22:23], 3, s[48:49]
	global_store_dwordx2 v[22:23], v[20:21], off
	v_add_u32_e32 v20, 0x2800, v14
	v_ashrrev_i32_e32 v21, 31, v20
	v_lshl_add_u64 v[20:21], v[20:21], 3, s[48:49]
	global_store_dwordx2 v[20:21], v[48:49], off
	v_add_u32_e32 v20, 0x2a00, v14
	v_ashrrev_i32_e32 v21, 31, v20
	v_lshl_add_u64 v[20:21], v[20:21], 3, s[48:49]
	global_store_dwordx2 v[20:21], v[40:41], off
	v_add_u32_e32 v20, 0x2c00, v14
	v_ashrrev_i32_e32 v21, 31, v20
	v_lshl_add_u64 v[20:21], v[20:21], 3, s[48:49]
	global_store_dwordx2 v[20:21], v[52:53], off
	v_add_u32_e32 v20, 0x2e00, v14
	v_ashrrev_i32_e32 v21, 31, v20
	v_lshl_add_u64 v[20:21], v[20:21], 3, s[48:49]
	global_store_dwordx2 v[20:21], v[42:43], off
	v_add_u32_e32 v20, 0x3000, v14
	v_ashrrev_i32_e32 v21, 31, v20
	v_lshl_add_u64 v[20:21], v[20:21], 3, s[48:49]
	global_store_dwordx2 v[20:21], v[46:47], off
	v_add_u32_e32 v20, 0x3200, v14
	v_ashrrev_i32_e32 v21, 31, v20
	v_lshl_add_u64 v[20:21], v[20:21], 3, s[48:49]
	global_store_dwordx2 v[20:21], v[32:33], off
	v_add_u32_e32 v20, 0x3400, v14
	v_ashrrev_i32_e32 v21, 31, v20
	v_lshl_add_u64 v[20:21], v[20:21], 3, s[48:49]
	global_store_dwordx2 v[20:21], v[44:45], off
	v_add_u32_e32 v20, 0x3600, v14
	v_ashrrev_i32_e32 v21, 31, v20
	v_lshl_add_u64 v[20:21], v[20:21], 3, s[48:49]
	global_store_dwordx2 v[20:21], v[30:31], off
	v_add_u32_e32 v20, 0x3800, v14
	v_ashrrev_i32_e32 v21, 31, v20
	v_lshl_add_u64 v[20:21], v[20:21], 3, s[48:49]
	global_store_dwordx2 v[20:21], v[34:35], off
	v_add_u32_e32 v20, 0x3a00, v14
	v_ashrrev_i32_e32 v21, 31, v20
	v_lshl_add_u64 v[20:21], v[20:21], 3, s[48:49]
	global_store_dwordx2 v[20:21], v[28:29], off
	v_add_u32_e32 v20, 0x3c00, v14
	v_add_u32_e32 v14, 0x3e00, v14
	v_ashrrev_i32_e32 v15, 31, v14
	v_ashrrev_i32_e32 v21, 31, v20
	v_lshl_add_u64 v[14:15], v[14:15], 3, s[48:49]
	v_lshl_add_u64 v[20:21], v[20:21], 3, s[48:49]
	global_store_dwordx2 v[14:15], v[18:19], off
	v_mov_b32_e32 v14, v1
	global_store_dwordx2 v[20:21], v[38:39], off
	s_barrier
	v_mov_b32_e32 v40, v170
	v_ashrrev_i32_e32 v15, 31, v14
	v_lshl_add_u64 v[18:19], v[14:15], 2, s[66:67]
	v_add_co_u32_e32 v28, vcc, s85, v18
	global_load_dword v20, v[18:19], off
	global_load_dword v21, v[18:19], off offset:2048
	v_addc_co_u32_e32 v29, vcc, 0, v19, vcc
	v_add_co_u32_e32 v22, vcc, s84, v18
	v_mov_b32_e32 v15, v174
	s_nop 0
	v_addc_co_u32_e32 v23, vcc, 0, v19, vcc
	v_add_co_u32_e32 v30, vcc, s61, v18
	v_mov_b32_e32 v45, v11
	s_nop 0
	v_addc_co_u32_e32 v31, vcc, 0, v19, vcc
	v_add_co_u32_e32 v32, vcc, s45, v18
	s_nop 1
	v_addc_co_u32_e32 v33, vcc, 0, v19, vcc
	v_add_co_u32_e32 v34, vcc, s88, v18
	global_load_dword v26, v[22:23], off offset:-4096
	global_load_dword v24, v[22:23], off
	global_load_dword v25, v[22:23], off offset:2048
	s_nop 0
	global_load_dword v22, v[32:33], off offset:-4096
	v_addc_co_u32_e32 v35, vcc, 0, v19, vcc
	v_add_co_u32_e32 v36, vcc, s0, v18
	s_mov_b32 s0, 0xa000
	s_nop 0
	v_addc_co_u32_e32 v37, vcc, 0, v19, vcc
	v_add_co_u32_e32 v38, vcc, s0, v18
	s_mov_b32 s0, 0x9000
	s_nop 0
	v_addc_co_u32_e32 v39, vcc, 0, v19, vcc
	global_load_dword v43, v[32:33], off offset:2048
	global_load_dword v46, v[34:35], off offset:-4096
	global_load_dword v48, v[36:37], off
	global_load_dword v49, v[36:37], off offset:2048
	global_load_dword v62, v[34:35], off
	global_load_dword v63, v[34:35], off offset:2048
	s_nop 0
	global_load_dword v34, v[38:39], off offset:-4096
	global_load_dword v64, v[36:37], off offset:-4096
	v_add_co_u32_e32 v36, vcc, s0, v18
	s_mov_b32 s0, 0xb000
	s_nop 0
	v_addc_co_u32_e32 v37, vcc, 0, v19, vcc
	global_load_dword v27, v[28:29], off offset:2048
	global_load_dword v35, v[36:37], off offset:2048
	v_add_co_u32_e32 v28, vcc, s86, v18
	global_load_dword v66, v[38:39], off
	global_load_dword v67, v[38:39], off offset:2048
	v_addc_co_u32_e32 v29, vcc, 0, v19, vcc
	v_add_co_u32_e32 v36, vcc, s0, v18
	s_mov_b32 s0, 0xc000
	s_nop 0
	v_addc_co_u32_e32 v37, vcc, 0, v19, vcc
	v_add_co_u32_e32 v38, vcc, s0, v18
	s_mov_b32 s0, 0xe000
	s_nop 0
	v_addc_co_u32_e32 v39, vcc, 0, v19, vcc
	global_load_dword v68, v[38:39], off offset:-4096
	global_load_dword v23, v[30:31], off offset:2048
	global_load_dword v69, v[36:37], off offset:2048
	v_add_co_u32_e32 v30, vcc, s90, v18
	s_waitcnt vmcnt(11)
	v_sub_f32_e32 v44, v21, v49
	v_addc_co_u32_e32 v31, vcc, 0, v19, vcc
	global_load_dword v47, v[28:29], off offset:2048
	global_load_dword v65, v[30:31], off offset:2048
	global_load_dword v42, v[32:33], off
	s_nop 0
	global_load_dword v30, v[38:39], off
	global_load_dword v31, v[38:39], off offset:2048
	v_add_co_u32_e32 v28, vcc, s0, v18
	s_mov_b32 s0, 0xd000
	s_nop 0
	v_addc_co_u32_e32 v29, vcc, 0, v19, vcc
	global_load_dword v32, v[28:29], off offset:-4096
	v_add_co_u32_e32 v36, vcc, s0, v18
	s_mov_b32 s0, 0xf000
	s_nop 0
	v_addc_co_u32_e32 v37, vcc, 0, v19, vcc
	global_load_dword v33, v[36:37], off offset:2048
	global_load_dword v38, v[28:29], off
	global_load_dword v39, v[28:29], off offset:2048
	v_add_co_u32_e32 v18, vcc, s0, v18
	v_mov_b32_e32 v36, v166
	s_nop 0
	v_addc_co_u32_e32 v19, vcc, 0, v19, vcc
	global_load_dword v70, v[18:19], off
	global_load_dword v71, v[18:19], off offset:2048
	v_mov_b32_e32 v28, v168
	v_mov_b32_e32 v13, v44
	s_nop 0
	v_mov_b32_e32 v10, v172
	v_pk_mul_f32 v[50:51], v[12:13], v[78:79] op_sel_hi:[1,0] neg_lo:[0,1] neg_hi:[0,1]
	s_waitcnt vmcnt(6)
	v_sub_f32_e32 v82, v43, v31
	v_pk_fma_f32 v[44:45], v[44:45], v[72:73], v[50:51] op_sel_hi:[1,0,1]
	v_sub_f32_e32 v50, v26, v34
	v_mov_b32_e32 v13, v50
	v_mov_b32_e32 v51, v11
	v_pk_mul_f32 v[52:53], v[12:13], v[40:41] op_sel_hi:[1,0] neg_lo:[0,1] neg_hi:[0,1]
	v_pk_mul_f32 v[84:85], v[82:83], v[78:79] op_sel_hi:[1,0] neg_lo:[0,1] neg_hi:[0,1]
	v_pk_fma_f32 v[50:51], v[50:51], v[36:37], v[52:53] op_sel_hi:[1,0,1]
	v_sub_f32_e32 v52, v27, v35
	v_mov_b32_e32 v13, v52
	v_mov_b32_e32 v53, v11
	v_pk_mul_f32 v[54:55], v[12:13], v[76:77] op_sel_hi:[1,0] neg_lo:[0,1] neg_hi:[0,1]
	v_sub_f32_e32 v10, v20, v48
	v_pk_fma_f32 v[54:55], v[52:53], v[74:75], v[54:55] op_sel_hi:[1,0,1]
	v_sub_f32_e32 v52, v24, v66
	v_mov_b32_e32 v13, v52
	v_pk_mul_f32 v[56:57], v[12:13], v[28:29] op_sel_hi:[1,0] neg_lo:[0,1] neg_hi:[0,1]
	v_pk_add_f32 v[20:21], v[20:21], v[48:49]
	v_pk_fma_f32 v[56:57], v[52:53], v[28:29], v[56:57] op_sel_hi:[1,0,1]
	v_sub_f32_e32 v52, v25, v67
	v_pk_mul_f32 v[58:59], v[52:53], v[76:77] op_sel_hi:[1,0]
	v_mov_b32_e32 v13, v52
	v_sub_f32_e32 v52, v22, v68
	v_pk_fma_f32 v[60:61], v[12:13], v[74:75], v[58:59] op_sel_hi:[1,0,1] neg_lo:[0,1,0] neg_hi:[0,1,0]
	v_pk_mul_f32 v[58:59], v[52:53], v[40:41] op_sel_hi:[1,0]
	v_mov_b32_e32 v13, v52
	v_sub_f32_e32 v52, v23, v69
	v_pk_fma_f32 v[58:59], v[12:13], v[36:37], v[58:59] op_sel_hi:[1,0,1] neg_lo:[0,1,0] neg_hi:[0,1,0]
	v_pk_mul_f32 v[80:81], v[52:53], v[78:79] op_sel_hi:[1,0]
	v_mov_b32_e32 v13, v52
	v_pk_fma_f32 v[52:53], v[12:13], v[72:73], v[80:81] op_sel_hi:[1,0,1] neg_lo:[0,1,0] neg_hi:[0,1,0]
	v_sub_f32_e32 v13, v42, v30
	v_xor_b32_e32 v81, 0x80000000, v13
	v_mov_b32_e32 v13, v82
	v_pk_fma_f32 v[82:83], v[12:13], v[72:73], v[84:85] op_sel_hi:[1,0,1] neg_lo:[0,1,0] neg_hi:[0,1,0]
	s_waitcnt vmcnt(5)
	v_sub_f32_e32 v84, v46, v32
	v_mov_b32_e32 v85, v11
	v_pk_mul_f32 v[86:87], v[84:85], v[40:41] op_sel_hi:[1,0] neg_lo:[0,1] neg_hi:[0,1]
	v_mov_b32_e32 v13, v84
	v_pk_fma_f32 v[84:85], v[12:13], v[36:37], v[86:87] op_sel_hi:[1,0,1] neg_lo:[0,1,0] neg_hi:[0,1,0]
	s_waitcnt vmcnt(4)
	v_sub_f32_e32 v86, v47, v33
	v_mov_b32_e32 v87, v11
	v_pk_mul_f32 v[88:89], v[86:87], v[76:77] op_sel_hi:[1,0] neg_lo:[0,1] neg_hi:[0,1]
	v_mov_b32_e32 v13, v86
	v_pk_fma_f32 v[86:87], v[12:13], v[74:75], v[88:89] op_sel_hi:[1,0,1] neg_lo:[0,1,0] neg_hi:[0,1,0]
	s_waitcnt vmcnt(3)
	v_sub_f32_e32 v88, v62, v38
	v_mov_b32_e32 v13, v88
	v_mov_b32_e32 v89, v11
	v_pk_mul_f32 v[90:91], v[12:13], v[28:29] op_sel_hi:[1,0] neg_lo:[0,1] neg_hi:[0,1]
	v_pk_add_f32 v[30:31], v[42:43], v[30:31]
	v_pk_fma_f32 v[88:89], v[88:89], v[28:29], v[90:91] op_sel_hi:[1,0,1] neg_lo:[0,1,0] neg_hi:[0,1,0]
	s_waitcnt vmcnt(2)
	v_sub_f32_e32 v90, v63, v39
	v_mov_b32_e32 v13, v90
	v_mov_b32_e32 v91, v11
	v_pk_mul_f32 v[76:77], v[12:13], v[76:77] op_sel_hi:[1,0] neg_lo:[0,1] neg_hi:[0,1]
	v_pk_add_f32 v[42:43], v[20:21], v[30:31] neg_lo:[0,1] neg_hi:[0,1]
	v_pk_fma_f32 v[74:75], v[90:91], v[74:75], v[76:77] op_sel_hi:[1,0,1] neg_lo:[0,1,0] neg_hi:[0,1,0]
	s_waitcnt vmcnt(1)
	v_sub_f32_e32 v76, v64, v70
	v_mov_b32_e32 v13, v76
	v_mov_b32_e32 v77, v11
	v_pk_mul_f32 v[90:91], v[12:13], v[40:41] op_sel_hi:[1,0] neg_lo:[0,1] neg_hi:[0,1]
	v_pk_add_f32 v[26:27], v[26:27], v[34:35]
	v_pk_fma_f32 v[76:77], v[76:77], v[36:37], v[90:91] op_sel_hi:[1,0,1] neg_lo:[0,1,0] neg_hi:[0,1,0]
	s_waitcnt vmcnt(0)
	v_sub_f32_e32 v90, v65, v71
	v_mov_b32_e32 v13, v90
	v_pk_mul_f32 v[78:79], v[12:13], v[78:79] op_sel_hi:[1,0] neg_lo:[0,1] neg_hi:[0,1]
	v_mov_b32_e32 v13, v43
	v_pk_add_f32 v[32:33], v[46:47], v[32:33]
	v_mov_b32_e32 v46, v42
	v_pk_add_f32 v[20:21], v[20:21], v[30:31]
	v_mov_b32_e32 v30, v43
	v_mov_b32_e32 v31, v11
	v_pk_mul_f32 v[42:43], v[12:13], v[40:41] op_sel_hi:[1,0] neg_lo:[0,1] neg_hi:[0,1]
	v_pk_add_f32 v[34:35], v[62:63], v[38:39]
	v_pk_fma_f32 v[62:63], v[30:31], v[36:37], v[42:43] op_sel_hi:[1,0,1]
	v_pk_add_f32 v[30:31], v[26:27], v[32:33] neg_lo:[0,1] neg_hi:[0,1]
	v_pk_add_f32 v[24:25], v[24:25], v[66:67]
	v_mov_b32_e32 v13, v30
	v_mov_b32_e32 v42, v30
	v_pk_mul_f32 v[48:49], v[12:13], v[28:29] op_sel_hi:[1,0] neg_lo:[0,1] neg_hi:[0,1]
	v_pk_add_f32 v[26:27], v[26:27], v[32:33]
	v_mov_b32_e32 v32, v31
	v_mov_b32_e32 v33, v11
	v_mov_b32_e32 v13, v31
	v_pk_add_f32 v[30:31], v[24:25], v[34:35] neg_lo:[0,1] neg_hi:[0,1]
	v_pk_add_f32 v[22:23], v[22:23], v[68:69]
	v_pk_add_f32 v[38:39], v[64:65], v[70:71]
	v_pk_mul_f32 v[32:33], v[32:33], v[40:41] op_sel_hi:[1,0]
	v_pk_add_f32 v[24:25], v[24:25], v[34:35]
	v_mov_b32_e32 v34, v31
	v_mov_b32_e32 v35, v11
	v_pk_fma_f32 v[32:33], v[12:13], v[36:37], v[32:33] op_sel_hi:[1,0,1] neg_lo:[0,1,0] neg_hi:[0,1,0]
	v_xor_b32_e32 v67, 0x80000000, v30
	v_pk_mul_f32 v[34:35], v[34:35], v[40:41] op_sel_hi:[1,0] neg_lo:[0,1] neg_hi:[0,1]
	v_mov_b32_e32 v13, v31
	v_pk_add_f32 v[30:31], v[22:23], v[38:39] neg_lo:[0,1] neg_hi:[0,1]
	v_mov_b32_e32 v43, v11
	v_pk_fma_f32 v[68:69], v[12:13], v[36:37], v[34:35] op_sel_hi:[1,0,1] neg_lo:[0,1,0] neg_hi:[0,1,0]
	v_mov_b32_e32 v13, v30
	v_pk_fma_f32 v[64:65], v[42:43], v[28:29], v[48:49] op_sel_hi:[1,0,1]
	v_mov_b32_e32 v34, v30
	v_mov_b32_e32 v35, v11
	v_pk_mul_f32 v[42:43], v[12:13], v[28:29] op_sel_hi:[1,0] neg_lo:[0,1] neg_hi:[0,1]
	v_mov_b32_e32 v13, v31
	v_pk_fma_f32 v[70:71], v[34:35], v[28:29], v[42:43] op_sel_hi:[1,0,1] neg_lo:[0,1,0] neg_hi:[0,1,0]
	v_mov_b32_e32 v34, v31
	v_pk_mul_f32 v[30:31], v[12:13], v[40:41] op_sel_hi:[1,0] neg_lo:[0,1] neg_hi:[0,1]
	v_pk_add_f32 v[22:23], v[22:23], v[38:39]
	v_pk_fma_f32 v[38:39], v[34:35], v[36:37], v[30:31] op_sel_hi:[1,0,1] neg_lo:[0,1,0] neg_hi:[0,1,0]
	v_pk_add_f32 v[30:31], v[20:21], v[24:25] neg_lo:[0,1] neg_hi:[0,1]
	v_pk_add_f32 v[20:21], v[20:21], v[24:25]
	v_mov_b32_e32 v13, v31
	v_mov_b32_e32 v42, v30
	v_mov_b32_e32 v24, v31
	v_mov_b32_e32 v25, v11
	v_pk_mul_f32 v[30:31], v[12:13], v[28:29] op_sel_hi:[1,0] neg_lo:[0,1] neg_hi:[0,1]
	v_mov_b32_e32 v91, v11
	v_pk_fma_f32 v[30:31], v[24:25], v[28:29], v[30:31] op_sel_hi:[1,0,1]
	v_pk_add_f32 v[24:25], v[26:27], v[22:23] neg_lo:[0,1] neg_hi:[0,1]
	v_pk_fma_f32 v[72:73], v[90:91], v[72:73], v[78:79] op_sel_hi:[1,0,1] neg_lo:[0,1,0] neg_hi:[0,1,0]
	v_mov_b32_e32 v13, v25
	v_xor_b32_e32 v79, 0x80000000, v24
	v_pk_add_f32 v[22:23], v[26:27], v[22:23]
	v_mov_b32_e32 v26, v25
	v_mov_b32_e32 v27, v11
	v_pk_mul_f32 v[24:25], v[12:13], v[28:29] op_sel_hi:[1,0] neg_lo:[0,1] neg_hi:[0,1]
	v_pk_add_f32 v[34:35], v[20:21], v[22:23]
	v_pk_fma_f32 v[26:27], v[26:27], v[28:29], v[24:25] op_sel_hi:[1,0,1] neg_lo:[0,1,0] neg_hi:[0,1,0]
	v_pk_add_f32 v[24:25], v[20:21], v[22:23] neg_lo:[0,1] neg_hi:[0,1]
	v_mov_b32_e32 v43, v11
	v_pk_add_f32 v[20:21], v[24:25], 0 neg_lo:[1,1] neg_hi:[1,1]
	v_mov_b32_e32 v78, v11
	v_mov_b32_e32 v90, v24
	v_mov_b32_e32 v20, v11
	v_pk_add_f32 v[48:49], v[90:91], v[20:21]
	v_pk_add_f32 v[24:25], v[90:91], v[20:21] neg_lo:[0,1] neg_hi:[0,1]
	v_pk_add_f32 v[20:21], v[42:43], v[78:79]
	v_pk_add_f32 v[22:23], v[42:43], v[78:79] neg_lo:[0,1] neg_hi:[0,1]
	v_pk_add_f32 v[42:43], v[30:31], v[26:27]
	v_pk_add_f32 v[26:27], v[30:31], v[26:27] neg_lo:[0,1] neg_hi:[0,1]
	v_mov_b32_e32 v47, v11
	v_mov_b32_e32 v66, v11
	v_xor_b32_e32 v79, 0x80000000, v26
	v_mov_b32_e32 v78, v27
	v_pk_add_f32 v[26:27], v[62:63], v[68:69]
	v_pk_add_f32 v[62:63], v[62:63], v[68:69] neg_lo:[0,1] neg_hi:[0,1]
	v_pk_add_f32 v[90:91], v[20:21], v[42:43]
	v_pk_add_f32 v[30:31], v[20:21], v[42:43] neg_lo:[0,1] neg_hi:[0,1]
	v_pk_add_f32 v[42:43], v[22:23], v[78:79]
	v_pk_add_f32 v[20:21], v[22:23], v[78:79] neg_lo:[0,1] neg_hi:[0,1]
	v_pk_add_f32 v[22:23], v[46:47], v[66:67]
	v_pk_add_f32 v[46:47], v[46:47], v[66:67] neg_lo:[0,1] neg_hi:[0,1]
	v_pk_mul_f32 v[66:67], v[28:29], v[62:63] op_sel:[0,1] op_sel_hi:[0,0] neg_lo:[1,1] neg_hi:[1,0]
	v_pk_fma_f32 v[66:67], v[28:29], v[62:63], v[66:67] op_sel_hi:[0,1,1]
	v_pk_add_f32 v[62:63], v[64:65], v[70:71]
	v_pk_add_f32 v[64:65], v[64:65], v[70:71] neg_lo:[0,1] neg_hi:[0,1]
	v_mov_b32_e32 v80, v11
	v_xor_b32_e32 v69, 0x80000000, v64
	v_mov_b32_e32 v68, v65
	v_pk_add_f32 v[64:65], v[32:33], v[38:39]
	v_pk_add_f32 v[32:33], v[32:33], v[38:39] neg_lo:[0,1] neg_hi:[0,1]
	v_pk_add_f32 v[78:79], v[44:45], v[82:83]
	v_pk_mul_f32 v[38:39], v[28:29], v[32:33] op_sel:[0,1] op_sel_hi:[0,0] neg_lo:[1,1] neg_hi:[1,0]
	v_pk_fma_f32 v[32:33], v[28:29], v[32:33], v[38:39] op_sel_hi:[0,1,1] neg_lo:[1,0,0] neg_hi:[1,0,0]
	v_pk_add_f32 v[38:39], v[22:23], v[62:63]
	v_pk_add_f32 v[22:23], v[22:23], v[62:63] neg_lo:[0,1] neg_hi:[0,1]
	v_pk_add_f32 v[62:63], v[26:27], v[64:65]
	v_pk_add_f32 v[26:27], v[26:27], v[64:65] neg_lo:[0,1] neg_hi:[0,1]
	v_pk_add_f32 v[70:71], v[38:39], v[62:63]
	v_pk_add_f32 v[38:39], v[38:39], v[62:63] neg_lo:[0,1] neg_hi:[0,1]
	v_pk_add_f32 v[62:63], v[22:23], v[26:27] op_sel:[0,1] op_sel_hi:[1,0] neg_hi:[0,1]
	v_pk_add_f32 v[26:27], v[22:23], v[26:27] op_sel:[0,1] op_sel_hi:[1,0] neg_lo:[0,1]
	v_pk_add_f32 v[22:23], v[46:47], v[68:69]
	v_pk_add_f32 v[64:65], v[46:47], v[68:69] neg_lo:[0,1] neg_hi:[0,1]
	v_pk_add_f32 v[46:47], v[66:67], v[32:33]
	v_pk_add_f32 v[32:33], v[66:67], v[32:33] neg_lo:[0,1] neg_hi:[0,1]
	v_pk_add_f32 v[44:45], v[44:45], v[82:83] neg_lo:[0,1] neg_hi:[0,1]
	v_xor_b32_e32 v67, 0x80000000, v32
	v_mov_b32_e32 v66, v33
	v_pk_add_f32 v[68:69], v[22:23], v[46:47]
	v_pk_add_f32 v[32:33], v[22:23], v[46:47] neg_lo:[0,1] neg_hi:[0,1]
	v_pk_add_f32 v[46:47], v[64:65], v[66:67]
	v_pk_add_f32 v[22:23], v[64:65], v[66:67] neg_lo:[0,1] neg_hi:[0,1]
	v_pk_add_f32 v[64:65], v[10:11], v[80:81]
	v_pk_add_f32 v[66:67], v[10:11], v[80:81] neg_lo:[0,1] neg_hi:[0,1]
	v_pk_mul_f32 v[80:81], v[40:41], v[44:45] op_sel:[0,1] op_sel_hi:[0,0] neg_lo:[1,1] neg_hi:[1,0]
	v_pk_fma_f32 v[44:45], v[36:37], v[44:45], v[80:81] op_sel_hi:[0,1,1]
	v_pk_add_f32 v[80:81], v[50:51], v[84:85]
	v_pk_add_f32 v[50:51], v[50:51], v[84:85] neg_lo:[0,1] neg_hi:[0,1]
	v_add_f32_e32 v10, v34, v35
	v_pk_mul_f32 v[82:83], v[28:29], v[50:51] op_sel:[0,1] op_sel_hi:[0,0] neg_lo:[1,1] neg_hi:[1,0]
	v_pk_fma_f32 v[82:83], v[28:29], v[50:51], v[82:83] op_sel_hi:[0,1,1]
	v_pk_add_f32 v[50:51], v[54:55], v[86:87]
	v_pk_add_f32 v[54:55], v[54:55], v[86:87] neg_lo:[0,1] neg_hi:[0,1]
	v_pk_fma_f32 v[16:17], v[10:11], s[42:43], v[16:17] op_sel_hi:[0,1,1]
	v_pk_mul_f32 v[84:85], v[36:37], v[54:55] op_sel:[0,1] op_sel_hi:[0,0] neg_lo:[1,1] neg_hi:[1,0]
	v_pk_fma_f32 v[84:85], v[40:41], v[54:55], v[84:85] op_sel_hi:[0,1,1]
	v_pk_add_f32 v[54:55], v[56:57], v[88:89]
	v_pk_add_f32 v[56:57], v[56:57], v[88:89] neg_lo:[0,1] neg_hi:[0,1]
	v_lshl_add_u32 v13, v15, 3, 0
	v_xor_b32_e32 v87, 0x80000000, v56
	v_mov_b32_e32 v86, v57
	v_pk_add_f32 v[56:57], v[60:61], v[74:75]
	v_pk_add_f32 v[60:61], v[60:61], v[74:75] neg_lo:[0,1] neg_hi:[0,1]
	ds_write_b64 v13, v[16:17]
	v_pk_mul_f32 v[74:75], v[36:37], v[60:61] op_sel:[0,1] op_sel_hi:[0,0] neg_lo:[1,1] neg_hi:[1,0]
	v_pk_fma_f32 v[60:61], v[40:41], v[60:61], v[74:75] op_sel_hi:[0,1,1] neg_lo:[1,0,0] neg_hi:[1,0,0]
	v_pk_add_f32 v[74:75], v[58:59], v[76:77]
	v_pk_add_f32 v[58:59], v[58:59], v[76:77] neg_lo:[0,1] neg_hi:[0,1]
	v_pk_fma_f32 v[16:17], v[180:181], s[92:93], v[180:181] op_sel:[1,0,0] op_sel_hi:[0,1,1]
	v_pk_mul_f32 v[76:77], v[28:29], v[58:59] op_sel:[0,1] op_sel_hi:[0,0] neg_lo:[1,1] neg_hi:[1,0]
	v_pk_fma_f32 v[58:59], v[28:29], v[58:59], v[76:77] op_sel_hi:[0,1,1] neg_lo:[1,0,0] neg_hi:[1,0,0]
	v_pk_add_f32 v[76:77], v[52:53], v[72:73]
	v_pk_add_f32 v[52:53], v[52:53], v[72:73] neg_lo:[0,1] neg_hi:[0,1]
	s_nop 0
	v_pk_mul_f32 v[40:41], v[40:41], v[52:53] op_sel:[0,1] op_sel_hi:[0,0] neg_lo:[1,1] neg_hi:[1,0]
	v_pk_fma_f32 v[52:53], v[36:37], v[52:53], v[40:41] op_sel_hi:[0,1,1] neg_lo:[1,0,0] neg_hi:[1,0,0]
	v_pk_add_f32 v[36:37], v[64:65], v[54:55]
	v_pk_add_f32 v[64:65], v[64:65], v[54:55] neg_lo:[0,1] neg_hi:[0,1]
	v_pk_add_f32 v[54:55], v[78:79], v[56:57] neg_lo:[0,1] neg_hi:[0,1]
	v_pk_add_f32 v[40:41], v[56:57], v[78:79]
	v_pk_mul_f32 v[56:57], v[28:29], v[54:55] op_sel:[0,1] op_sel_hi:[0,0] neg_lo:[1,1] neg_hi:[1,0]
	v_pk_add_f32 v[72:73], v[80:81], v[74:75] neg_lo:[0,1] neg_hi:[0,1]
	v_pk_fma_f32 v[56:57], v[28:29], v[54:55], v[56:57] op_sel_hi:[0,1,1]
	v_pk_add_f32 v[54:55], v[80:81], v[74:75]
	v_xor_b32_e32 v75, 0x80000000, v72
	v_mov_b32_e32 v74, v73
	v_pk_add_f32 v[72:73], v[50:51], v[76:77]
	v_pk_add_f32 v[50:51], v[50:51], v[76:77] neg_lo:[0,1] neg_hi:[0,1]
	s_nop 0
	v_pk_mul_f32 v[76:77], v[28:29], v[50:51] op_sel:[0,1] op_sel_hi:[0,0] neg_lo:[1,1] neg_hi:[1,0]
	v_pk_fma_f32 v[50:51], v[28:29], v[50:51], v[76:77] op_sel_hi:[0,1,1] neg_lo:[1,0,0] neg_hi:[1,0,0]
	v_pk_add_f32 v[76:77], v[36:37], v[54:55]
	v_pk_add_f32 v[36:37], v[36:37], v[54:55] neg_lo:[0,1] neg_hi:[0,1]
	v_pk_add_f32 v[54:55], v[40:41], v[72:73]
	v_pk_add_f32 v[40:41], v[40:41], v[72:73] neg_lo:[0,1] neg_hi:[0,1]
	v_pk_add_f32 v[78:79], v[76:77], v[54:55]
	v_pk_add_f32 v[54:55], v[76:77], v[54:55] neg_lo:[0,1] neg_hi:[0,1]
	v_pk_add_f32 v[76:77], v[36:37], v[40:41] op_sel:[0,1] op_sel_hi:[1,0] neg_hi:[0,1]
	v_pk_add_f32 v[40:41], v[36:37], v[40:41] op_sel:[0,1] op_sel_hi:[1,0] neg_lo:[0,1]
	v_pk_add_f32 v[72:73], v[56:57], v[50:51]
	v_pk_add_f32 v[50:51], v[56:57], v[50:51] neg_lo:[0,1] neg_hi:[0,1]
	v_pk_add_f32 v[36:37], v[64:65], v[74:75]
	v_pk_add_f32 v[64:65], v[64:65], v[74:75] neg_lo:[0,1] neg_hi:[0,1]
	v_xor_b32_e32 v57, 0x80000000, v50
	v_mov_b32_e32 v56, v51
	v_pk_add_f32 v[74:75], v[36:37], v[72:73]
	v_pk_add_f32 v[50:51], v[36:37], v[72:73] neg_lo:[0,1] neg_hi:[0,1]
	v_pk_add_f32 v[72:73], v[64:65], v[56:57]
	v_pk_add_f32 v[36:37], v[64:65], v[56:57] neg_lo:[0,1] neg_hi:[0,1]
	v_pk_add_f32 v[56:57], v[66:67], v[86:87]
	v_pk_add_f32 v[64:65], v[66:67], v[86:87] neg_lo:[0,1] neg_hi:[0,1]
	v_pk_add_f32 v[66:67], v[60:61], v[44:45]
	v_pk_add_f32 v[44:45], v[44:45], v[60:61] neg_lo:[0,1] neg_hi:[0,1]
	s_nop 0
	v_pk_mul_f32 v[60:61], v[28:29], v[44:45] op_sel:[0,1] op_sel_hi:[0,0] neg_lo:[1,1] neg_hi:[1,0]
	v_pk_fma_f32 v[60:61], v[28:29], v[44:45], v[60:61] op_sel_hi:[0,1,1]
	v_pk_add_f32 v[44:45], v[82:83], v[58:59]
	v_pk_add_f32 v[58:59], v[82:83], v[58:59] neg_lo:[0,1] neg_hi:[0,1]
	s_nop 0
	v_xor_b32_e32 v81, 0x80000000, v58
	v_mov_b32_e32 v80, v59
	v_pk_add_f32 v[58:59], v[84:85], v[52:53]
	v_pk_add_f32 v[52:53], v[84:85], v[52:53] neg_lo:[0,1] neg_hi:[0,1]
	s_nop 0
	v_pk_mul_f32 v[82:83], v[28:29], v[52:53] op_sel:[0,1] op_sel_hi:[0,0] neg_lo:[1,1] neg_hi:[1,0]
	v_pk_fma_f32 v[28:29], v[28:29], v[52:53], v[82:83] op_sel_hi:[0,1,1] neg_lo:[1,0,0] neg_hi:[1,0,0]
	v_pk_add_f32 v[52:53], v[56:57], v[44:45]
	v_pk_add_f32 v[44:45], v[56:57], v[44:45] neg_lo:[0,1] neg_hi:[0,1]
	v_pk_add_f32 v[56:57], v[66:67], v[58:59]
	v_pk_add_f32 v[58:59], v[66:67], v[58:59] neg_lo:[0,1] neg_hi:[0,1]
	s_nop 0
	v_pk_add_f32 v[82:83], v[44:45], v[58:59] op_sel:[0,1] op_sel_hi:[1,0] neg_hi:[0,1]
	v_pk_add_f32 v[44:45], v[44:45], v[58:59] op_sel:[0,1] op_sel_hi:[1,0] neg_lo:[0,1]
	v_pk_add_f32 v[66:67], v[60:61], v[28:29]
	v_pk_add_f32 v[28:29], v[60:61], v[28:29] neg_lo:[0,1] neg_hi:[0,1]
	v_pk_add_f32 v[58:59], v[52:53], v[56:57]
	v_pk_add_f32 v[56:57], v[52:53], v[56:57] neg_lo:[0,1] neg_hi:[0,1]
	v_pk_add_f32 v[52:53], v[64:65], v[80:81]
	v_pk_add_f32 v[64:65], v[64:65], v[80:81] neg_lo:[0,1] neg_hi:[0,1]
	v_pk_add_f32 v[80:81], v[52:53], v[66:67]
	v_pk_add_f32 v[52:53], v[52:53], v[66:67] neg_lo:[0,1] neg_hi:[0,1]
	v_pk_add_f32 v[66:67], v[64:65], v[28:29] op_sel:[0,1] op_sel_hi:[1,0] neg_hi:[0,1]
	v_pk_add_f32 v[28:29], v[64:65], v[28:29] op_sel:[0,1] op_sel_hi:[1,0] neg_lo:[0,1]
	v_pk_mul_f32 v[60:61], v[16:17], v[78:79] op_sel:[1,1] op_sel_hi:[0,1] neg_lo:[0,1]
	v_pk_fma_f32 v[60:61], v[16:17], v[78:79], v[60:61] op_sel_hi:[1,0,1]
	ds_write_b64 v13, v[60:61] offset:4224
	v_pk_mul_f32 v[60:61], v[180:181], v[16:17] op_sel:[1,1] op_sel_hi:[0,1] neg_lo:[0,1]
	v_pk_fma_f32 v[16:17], v[180:181], v[16:17], v[60:61] op_sel_hi:[1,0,1]
	s_nop 0
	v_pk_mul_f32 v[60:61], v[16:17], v[70:71] op_sel:[1,1] op_sel_hi:[0,1] neg_lo:[0,1]
	v_pk_fma_f32 v[60:61], v[16:17], v[70:71], v[60:61] op_sel_hi:[1,0,1]
	ds_write_b64 v13, v[60:61] offset:8448
	v_pk_mul_f32 v[60:61], v[180:181], v[16:17] op_sel:[1,1] op_sel_hi:[0,1] neg_lo:[0,1]
	v_pk_fma_f32 v[16:17], v[180:181], v[16:17], v[60:61] op_sel_hi:[1,0,1]
	s_nop 0
	v_pk_mul_f32 v[60:61], v[16:17], v[58:59] op_sel:[1,1] op_sel_hi:[0,1] neg_lo:[0,1]
	v_pk_fma_f32 v[58:59], v[16:17], v[58:59], v[60:61] op_sel_hi:[1,0,1]
	ds_write_b64 v13, v[58:59] offset:12672
	v_pk_mul_f32 v[58:59], v[180:181], v[16:17] op_sel:[1,1] op_sel_hi:[0,1] neg_lo:[0,1]
	v_pk_fma_f32 v[16:17], v[180:181], v[16:17], v[58:59] op_sel_hi:[1,0,1]
	s_nop 0
	v_pk_mul_f32 v[58:59], v[90:91], v[16:17] op_sel:[1,1] op_sel_hi:[1,0] neg_lo:[1,0]
	s_nop 0
	v_pk_fma_f32 v[58:59], v[90:91], v[16:17], v[58:59] op_sel_hi:[0,1,1]
	ds_write_b64 v13, v[58:59] offset:16896
	v_pk_mul_f32 v[58:59], v[180:181], v[16:17] op_sel:[1,1] op_sel_hi:[0,1] neg_lo:[0,1]
	v_pk_fma_f32 v[16:17], v[180:181], v[16:17], v[58:59] op_sel_hi:[1,0,1]
	s_nop 0
	v_pk_mul_f32 v[58:59], v[16:17], v[74:75] op_sel:[1,1] op_sel_hi:[0,1] neg_lo:[0,1]
	v_pk_fma_f32 v[58:59], v[16:17], v[74:75], v[58:59] op_sel_hi:[1,0,1]
	ds_write_b64 v13, v[58:59] offset:21120
	v_pk_mul_f32 v[58:59], v[180:181], v[16:17] op_sel:[1,1] op_sel_hi:[0,1] neg_lo:[0,1]
	v_pk_fma_f32 v[16:17], v[180:181], v[16:17], v[58:59] op_sel_hi:[1,0,1]
	s_nop 0
	v_pk_mul_f32 v[58:59], v[68:69], v[16:17] op_sel:[1,1] op_sel_hi:[1,0] neg_lo:[1,0]
	s_nop 0
	v_pk_fma_f32 v[58:59], v[68:69], v[16:17], v[58:59] op_sel_hi:[0,1,1]
	ds_write_b64 v13, v[58:59] offset:25344
	v_pk_mul_f32 v[58:59], v[180:181], v[16:17] op_sel:[1,1] op_sel_hi:[0,1] neg_lo:[0,1]
	v_pk_fma_f32 v[16:17], v[180:181], v[16:17], v[58:59] op_sel_hi:[1,0,1]
	s_nop 0
	v_pk_mul_f32 v[58:59], v[80:81], v[16:17] op_sel:[1,1] op_sel_hi:[1,0] neg_lo:[1,0]
	s_nop 0
	v_pk_fma_f32 v[58:59], v[80:81], v[16:17], v[58:59] op_sel_hi:[0,1,1]
	ds_write_b64 v13, v[58:59] offset:29568
	v_pk_mul_f32 v[58:59], v[180:181], v[16:17] op_sel:[1,1] op_sel_hi:[0,1] neg_lo:[0,1]
	v_pk_fma_f32 v[16:17], v[180:181], v[16:17], v[58:59] op_sel_hi:[1,0,1]
	s_nop 0
	v_pk_mul_f32 v[58:59], v[48:49], v[16:17] op_sel:[1,1] op_sel_hi:[1,0] neg_lo:[1,0]
	s_nop 0
	v_pk_fma_f32 v[48:49], v[48:49], v[16:17], v[58:59] op_sel_hi:[0,1,1]
	ds_write_b64 v13, v[48:49] offset:33792
	v_pk_mul_f32 v[48:49], v[180:181], v[16:17] op_sel:[1,1] op_sel_hi:[0,1] neg_lo:[0,1]
	v_pk_fma_f32 v[16:17], v[180:181], v[16:17], v[48:49] op_sel_hi:[1,0,1]
	s_nop 0
	v_pk_mul_f32 v[48:49], v[76:77], v[16:17] op_sel:[1,1] op_sel_hi:[1,0] neg_lo:[1,0]
	s_nop 0
	v_pk_fma_f32 v[48:49], v[76:77], v[16:17], v[48:49] op_sel_hi:[0,1,1]
	ds_write_b64 v13, v[48:49] offset:38016
	v_pk_mul_f32 v[48:49], v[180:181], v[16:17] op_sel:[1,1] op_sel_hi:[0,1] neg_lo:[0,1]
	v_pk_fma_f32 v[16:17], v[180:181], v[16:17], v[48:49] op_sel_hi:[1,0,1]
	s_nop 0
	v_pk_mul_f32 v[48:49], v[62:63], v[16:17] op_sel:[1,1] op_sel_hi:[1,0] neg_lo:[1,0]
	s_nop 0
	v_pk_fma_f32 v[48:49], v[62:63], v[16:17], v[48:49] op_sel_hi:[0,1,1]
	ds_write_b64 v13, v[48:49] offset:42240
	v_pk_mul_f32 v[48:49], v[180:181], v[16:17] op_sel:[1,1] op_sel_hi:[0,1] neg_lo:[0,1]
	v_pk_fma_f32 v[16:17], v[180:181], v[16:17], v[48:49] op_sel_hi:[1,0,1]
	s_nop 0
	v_pk_mul_f32 v[48:49], v[82:83], v[16:17] op_sel:[1,1] op_sel_hi:[1,0] neg_lo:[1,0]
	s_nop 0
	v_pk_fma_f32 v[48:49], v[82:83], v[16:17], v[48:49] op_sel_hi:[0,1,1]
	ds_write_b64 v13, v[48:49] offset:46464
	v_pk_mul_f32 v[48:49], v[180:181], v[16:17] op_sel:[1,1] op_sel_hi:[0,1] neg_lo:[0,1]
	v_pk_fma_f32 v[16:17], v[180:181], v[16:17], v[48:49] op_sel_hi:[1,0,1]
	s_nop 0
	v_pk_mul_f32 v[48:49], v[42:43], v[16:17] op_sel:[1,1] op_sel_hi:[1,0] neg_lo:[1,0]
	s_nop 0
	v_pk_fma_f32 v[42:43], v[42:43], v[16:17], v[48:49] op_sel_hi:[0,1,1]
	ds_write_b64 v13, v[42:43] offset:50688
	v_pk_mul_f32 v[42:43], v[180:181], v[16:17] op_sel:[1,1] op_sel_hi:[0,1] neg_lo:[0,1]
	v_pk_fma_f32 v[16:17], v[180:181], v[16:17], v[42:43] op_sel_hi:[1,0,1]
	s_nop 0
	v_pk_mul_f32 v[42:43], v[72:73], v[16:17] op_sel:[1,1] op_sel_hi:[1,0] neg_lo:[1,0]
	s_nop 0
	v_pk_fma_f32 v[42:43], v[72:73], v[16:17], v[42:43] op_sel_hi:[0,1,1]
	ds_write_b64 v13, v[42:43] offset:54912
	v_pk_mul_f32 v[42:43], v[180:181], v[16:17] op_sel:[1,1] op_sel_hi:[0,1] neg_lo:[0,1]
	v_pk_fma_f32 v[16:17], v[180:181], v[16:17], v[42:43] op_sel_hi:[1,0,1]
	s_nop 0
	v_pk_mul_f32 v[42:43], v[46:47], v[16:17] op_sel:[1,1] op_sel_hi:[1,0] neg_lo:[1,0]
	s_nop 0
	v_pk_fma_f32 v[42:43], v[46:47], v[16:17], v[42:43] op_sel_hi:[0,1,1]
	ds_write_b64 v13, v[42:43] offset:59136
	v_pk_mul_f32 v[42:43], v[180:181], v[16:17] op_sel:[1,1] op_sel_hi:[0,1] neg_lo:[0,1]
	v_pk_fma_f32 v[16:17], v[180:181], v[16:17], v[42:43] op_sel_hi:[1,0,1]
	s_nop 0
	v_pk_mul_f32 v[42:43], v[66:67], v[16:17] op_sel:[1,1] op_sel_hi:[1,0] neg_lo:[1,0]
	s_nop 0
	v_pk_fma_f32 v[42:43], v[66:67], v[16:17], v[42:43] op_sel_hi:[0,1,1]
	ds_write_b64 v13, v[42:43] offset:63360
	v_pk_mul_f32 v[42:43], v[180:181], v[16:17] op_sel:[1,1] op_sel_hi:[0,1] neg_lo:[0,1]
	v_pk_fma_f32 v[16:17], v[180:181], v[16:17], v[42:43] op_sel_hi:[1,0,1]
	v_sub_f32_e32 v10, v34, v35
	v_pk_mul_f32 v[34:35], v[16:17], s[46:47]
	s_nop 0
	v_pk_fma_f32 v[34:35], v[10:11], v[16:17], v[34:35] op_sel:[0,0,1] op_sel_hi:[0,1,0]
	v_add_u32_e32 v10, 0x10800, v13
	ds_write_b64 v10, v[34:35]
	v_pk_mul_f32 v[34:35], v[180:181], v[16:17] op_sel:[1,1] op_sel_hi:[0,1] neg_lo:[0,1]
	v_pk_fma_f32 v[16:17], v[180:181], v[16:17], v[34:35] op_sel_hi:[1,0,1]
	s_nop 0
	v_pk_mul_f32 v[34:35], v[54:55], v[16:17] op_sel:[1,1] op_sel_hi:[1,0] neg_lo:[1,0]
	v_add_u32_e32 v10, 0x11880, v13
	v_pk_fma_f32 v[34:35], v[54:55], v[16:17], v[34:35] op_sel_hi:[0,1,1]
	ds_write_b64 v10, v[34:35]
	v_pk_mul_f32 v[34:35], v[180:181], v[16:17] op_sel:[1,1] op_sel_hi:[0,1] neg_lo:[0,1]
	v_pk_fma_f32 v[16:17], v[180:181], v[16:17], v[34:35] op_sel_hi:[1,0,1]
	s_nop 0
	v_pk_mul_f32 v[34:35], v[38:39], v[16:17] op_sel:[1,1] op_sel_hi:[1,0] neg_lo:[1,0]
	v_add_u32_e32 v10, 0x12900, v13
	v_pk_fma_f32 v[34:35], v[38:39], v[16:17], v[34:35] op_sel_hi:[0,1,1]
	ds_write_b64 v10, v[34:35]
	v_pk_mul_f32 v[34:35], v[180:181], v[16:17] op_sel:[1,1] op_sel_hi:[0,1] neg_lo:[0,1]
	v_pk_fma_f32 v[16:17], v[180:181], v[16:17], v[34:35] op_sel_hi:[1,0,1]
	s_nop 0
	v_pk_mul_f32 v[34:35], v[56:57], v[16:17] op_sel:[1,1] op_sel_hi:[1,0] neg_lo:[1,0]
	v_add_u32_e32 v10, 0x13980, v13
	v_pk_fma_f32 v[34:35], v[56:57], v[16:17], v[34:35] op_sel_hi:[0,1,1]
	ds_write_b64 v10, v[34:35]
	v_pk_mul_f32 v[34:35], v[180:181], v[16:17] op_sel:[1,1] op_sel_hi:[0,1] neg_lo:[0,1]
	v_pk_fma_f32 v[16:17], v[180:181], v[16:17], v[34:35] op_sel_hi:[1,0,1]
	s_nop 0
	v_pk_mul_f32 v[34:35], v[30:31], v[16:17] op_sel:[1,1] op_sel_hi:[1,0] neg_lo:[1,0]
	v_add_u32_e32 v10, 0x14a00, v13
	v_pk_fma_f32 v[30:31], v[30:31], v[16:17], v[34:35] op_sel_hi:[0,1,1]
	ds_write_b64 v10, v[30:31]
	v_pk_mul_f32 v[30:31], v[180:181], v[16:17] op_sel:[1,1] op_sel_hi:[0,1] neg_lo:[0,1]
	v_pk_fma_f32 v[16:17], v[180:181], v[16:17], v[30:31] op_sel_hi:[1,0,1]
	s_nop 0
	v_pk_mul_f32 v[30:31], v[50:51], v[16:17] op_sel:[1,1] op_sel_hi:[1,0] neg_lo:[1,0]
	v_add_u32_e32 v10, 0x15a80, v13
	v_pk_fma_f32 v[30:31], v[50:51], v[16:17], v[30:31] op_sel_hi:[0,1,1]
	ds_write_b64 v10, v[30:31]
	v_pk_mul_f32 v[30:31], v[180:181], v[16:17] op_sel:[1,1] op_sel_hi:[0,1] neg_lo:[0,1]
	v_pk_fma_f32 v[16:17], v[180:181], v[16:17], v[30:31] op_sel_hi:[1,0,1]
	s_nop 0
	v_pk_mul_f32 v[30:31], v[32:33], v[16:17] op_sel:[1,1] op_sel_hi:[1,0] neg_lo:[1,0]
	v_add_u32_e32 v10, 0x16b00, v13
	v_pk_fma_f32 v[30:31], v[32:33], v[16:17], v[30:31] op_sel_hi:[0,1,1]
	ds_write_b64 v10, v[30:31]
	v_pk_mul_f32 v[30:31], v[180:181], v[16:17] op_sel:[1,1] op_sel_hi:[0,1] neg_lo:[0,1]
	v_pk_fma_f32 v[16:17], v[180:181], v[16:17], v[30:31] op_sel_hi:[1,0,1]
	s_nop 0
	v_pk_mul_f32 v[30:31], v[52:53], v[16:17] op_sel:[1,1] op_sel_hi:[1,0] neg_lo:[1,0]
	v_add_u32_e32 v10, 0x17b80, v13
	v_pk_fma_f32 v[30:31], v[52:53], v[16:17], v[30:31] op_sel_hi:[0,1,1]
	ds_write_b64 v10, v[30:31]
	v_pk_mul_f32 v[30:31], v[180:181], v[16:17] op_sel:[1,1] op_sel_hi:[0,1] neg_lo:[0,1]
	v_pk_fma_f32 v[16:17], v[180:181], v[16:17], v[30:31] op_sel_hi:[1,0,1]
	s_nop 0
	v_pk_mul_f32 v[30:31], v[24:25], v[16:17] op_sel:[1,1] op_sel_hi:[1,0] neg_lo:[1,0]
	v_add_u32_e32 v10, 0x18c00, v13
	v_pk_fma_f32 v[24:25], v[24:25], v[16:17], v[30:31] op_sel_hi:[0,1,1]
	ds_write_b64 v10, v[24:25]
	v_pk_mul_f32 v[24:25], v[180:181], v[16:17] op_sel:[1,1] op_sel_hi:[0,1] neg_lo:[0,1]
	v_pk_fma_f32 v[16:17], v[180:181], v[16:17], v[24:25] op_sel_hi:[1,0,1]
	s_nop 0
	v_pk_mul_f32 v[24:25], v[40:41], v[16:17] op_sel:[1,1] op_sel_hi:[1,0] neg_lo:[1,0]
	v_add_u32_e32 v10, 0x19c80, v13
	v_pk_fma_f32 v[24:25], v[40:41], v[16:17], v[24:25] op_sel_hi:[0,1,1]
	ds_write_b64 v10, v[24:25]
	v_pk_mul_f32 v[24:25], v[180:181], v[16:17] op_sel:[1,1] op_sel_hi:[0,1] neg_lo:[0,1]
	v_pk_fma_f32 v[16:17], v[180:181], v[16:17], v[24:25] op_sel_hi:[1,0,1]
	s_nop 0
	v_pk_mul_f32 v[24:25], v[26:27], v[16:17] op_sel:[1,1] op_sel_hi:[1,0] neg_lo:[1,0]
	v_add_u32_e32 v10, 0x1ad00, v13
	v_pk_fma_f32 v[24:25], v[26:27], v[16:17], v[24:25] op_sel_hi:[0,1,1]
	ds_write_b64 v10, v[24:25]
	v_pk_mul_f32 v[24:25], v[180:181], v[16:17] op_sel:[1,1] op_sel_hi:[0,1] neg_lo:[0,1]
	v_pk_fma_f32 v[16:17], v[180:181], v[16:17], v[24:25] op_sel_hi:[1,0,1]
	s_nop 0
	v_pk_mul_f32 v[24:25], v[44:45], v[16:17] op_sel:[1,1] op_sel_hi:[1,0] neg_lo:[1,0]
	v_add_u32_e32 v10, 0x1bd80, v13
	v_pk_fma_f32 v[24:25], v[44:45], v[16:17], v[24:25] op_sel_hi:[0,1,1]
	ds_write_b64 v10, v[24:25]
	v_pk_mul_f32 v[24:25], v[180:181], v[16:17] op_sel:[1,1] op_sel_hi:[0,1] neg_lo:[0,1]
	v_pk_fma_f32 v[16:17], v[180:181], v[16:17], v[24:25] op_sel_hi:[1,0,1]
	s_nop 0
	v_pk_mul_f32 v[24:25], v[20:21], v[16:17] op_sel:[1,1] op_sel_hi:[1,0] neg_lo:[1,0]
	v_add_u32_e32 v10, 0x1ce00, v13
	v_pk_fma_f32 v[20:21], v[20:21], v[16:17], v[24:25] op_sel_hi:[0,1,1]
	ds_write_b64 v10, v[20:21]
	v_pk_mul_f32 v[20:21], v[180:181], v[16:17] op_sel:[1,1] op_sel_hi:[0,1] neg_lo:[0,1]
	v_pk_fma_f32 v[16:17], v[180:181], v[16:17], v[20:21] op_sel_hi:[1,0,1]
	s_nop 0
	v_pk_mul_f32 v[20:21], v[36:37], v[16:17] op_sel:[1,1] op_sel_hi:[1,0] neg_lo:[1,0]
	v_add_u32_e32 v10, 0x1de80, v13
	v_pk_fma_f32 v[20:21], v[36:37], v[16:17], v[20:21] op_sel_hi:[0,1,1]
	ds_write_b64 v10, v[20:21]
	v_pk_mul_f32 v[20:21], v[180:181], v[16:17] op_sel:[1,1] op_sel_hi:[0,1] neg_lo:[0,1]
	v_pk_fma_f32 v[16:17], v[180:181], v[16:17], v[20:21] op_sel_hi:[1,0,1]
	s_nop 0
	v_pk_mul_f32 v[20:21], v[22:23], v[16:17] op_sel:[1,1] op_sel_hi:[1,0] neg_lo:[1,0]
	v_add_u32_e32 v10, 0x1ef00, v13
	v_pk_fma_f32 v[20:21], v[22:23], v[16:17], v[20:21] op_sel_hi:[0,1,1]
	ds_write_b64 v10, v[20:21]
	v_pk_mul_f32 v[20:21], v[180:181], v[16:17] op_sel:[1,1] op_sel_hi:[0,1] neg_lo:[0,1]
	v_pk_fma_f32 v[16:17], v[180:181], v[16:17], v[20:21] op_sel_hi:[1,0,1]
	s_nop 0
	v_pk_mul_f32 v[18:19], v[28:29], v[16:17] op_sel:[1,1] op_sel_hi:[1,0] neg_lo:[1,0]
	v_add_u32_e32 v10, 0x1ff80, v13
	v_pk_fma_f32 v[16:17], v[28:29], v[16:17], v[18:19] op_sel_hi:[0,1,1]
	ds_write_b64 v10, v[16:17]
	v_mov_b32_e32 v10, v176
	v_mov_b32_e32 v13, v173
	s_waitcnt lgkmcnt(0)
	s_barrier
	v_mov_b32_e32 v16, v182
	v_add_u32_e32 v15, v13, v10
	v_lshl_add_u32 v75, v15, 3, 0
	v_xad_u32 v15, v13, 1, v10
	v_lshl_add_u32 v74, v15, 3, 0
	v_xad_u32 v15, v13, 2, v10
	v_lshl_add_u32 v73, v15, 3, 0
	v_xad_u32 v15, v13, 3, v10
	v_lshl_add_u32 v72, v15, 3, 0
	v_xad_u32 v15, v13, 4, v10
	v_lshl_add_u32 v71, v15, 3, 0
	v_xad_u32 v15, v13, 5, v10
	v_lshl_add_u32 v70, v15, 3, 0
	v_xad_u32 v15, v13, 6, v10
	v_lshl_add_u32 v69, v15, 3, 0
	v_xad_u32 v15, v13, 7, v10
	v_lshl_add_u32 v68, v15, 3, 0
	v_xad_u32 v15, v13, 8, v10
	v_lshl_add_u32 v15, v15, 3, 0
	v_add_u32_e32 v67, 0x800, v15
	v_xad_u32 v15, v13, 9, v10
	v_lshl_add_u32 v15, v15, 3, 0
	v_add_u32_e32 v66, 0x800, v15
	v_xad_u32 v15, v13, 10, v10
	v_lshl_add_u32 v15, v15, 3, 0
	v_add_u32_e32 v65, 0x800, v15
	v_xad_u32 v15, v13, 11, v10
	v_lshl_add_u32 v15, v15, 3, 0
	v_add_u32_e32 v64, 0x800, v15
	v_xad_u32 v15, v13, 12, v10
	v_mov_b32_e32 v17, v183
	v_lshl_add_u32 v15, v15, 3, 0
	ds_read2_b64 v[18:21], v75 offset1:16
	ds_read2_b64 v[40:43], v67 offset1:16
	v_add_u32_e32 v63, 0x800, v15
	v_xad_u32 v15, v13, 13, v10
	v_lshl_add_u32 v15, v15, 3, 0
	v_add_u32_e32 v62, 0x800, v15
	v_xad_u32 v15, v13, 14, v10
	v_xad_u32 v10, v13, 15, v10
	ds_read2_b64 v[22:25], v74 offset0:32 offset1:48
	ds_read2_b64 v[48:51], v66 offset0:32 offset1:48
	v_lshl_add_u32 v15, v15, 3, 0
	v_lshl_add_u32 v10, v10, 3, 0
	v_add_u32_e32 v15, 0x800, v15
	v_add_u32_e32 v13, 0x800, v10
	v_mov_b32_e32 v10, v164
	ds_read2_b64 v[26:29], v73 offset0:64 offset1:80
	ds_read2_b64 v[58:61], v72 offset0:96 offset1:112
	ds_read2_b64 v[76:79], v71 offset0:128 offset1:144
	ds_read2_b64 v[80:83], v70 offset0:160 offset1:176
	ds_read2_b64 v[84:87], v69 offset0:192 offset1:208
	ds_read2_b64 v[88:91], v68 offset0:224 offset1:240
	ds_read2_b64 v[54:57], v65 offset0:64 offset1:80
	ds_read2_b64 v[92:95], v64 offset0:96 offset1:112
	ds_read2_b64 v[96:99], v63 offset0:128 offset1:144
	ds_read2_b64 v[100:103], v62 offset0:160 offset1:176
	ds_read2_b64 v[104:107], v15 offset0:192 offset1:208
	ds_read2_b64 v[108:111], v13 offset0:224 offset1:240
	s_waitcnt lgkmcnt(14)
	v_pk_add_f32 v[112:113], v[18:19], v[40:41]
	v_pk_add_f32 v[40:41], v[18:19], v[40:41] neg_lo:[0,1] neg_hi:[0,1]
	v_pk_add_f32 v[18:19], v[20:21], v[42:43]
	v_pk_add_f32 v[20:21], v[20:21], v[42:43] neg_lo:[0,1] neg_hi:[0,1]
	v_mov_b32_e32 v30, v165
	v_mov_b32_e32 v32, v166
	v_mov_b32_e32 v34, v167
	v_mov_b32_e32 v10, v168
	v_mov_b32_e32 v38, v169
	v_mov_b32_e32 v36, v170
	v_mov_b32_e32 v46, v171
	v_mov_b32_e32 v31, v172
	v_pk_mul_f32 v[42:43], v[20:21], v[46:47] op_sel:[1,0] op_sel_hi:[0,0] neg_lo:[1,1] neg_hi:[0,1]
	s_nop 0
	v_pk_fma_f32 v[44:45], v[20:21], v[30:31], v[42:43] op_sel_hi:[1,0,1]
	s_waitcnt lgkmcnt(12)
	v_pk_add_f32 v[20:21], v[22:23], v[48:49]
	v_pk_add_f32 v[22:23], v[22:23], v[48:49] neg_lo:[0,1] neg_hi:[0,1]
	s_nop 0
	v_pk_mul_f32 v[42:43], v[22:23], v[36:37] op_sel:[1,0] op_sel_hi:[0,0] neg_lo:[1,1] neg_hi:[0,1]
	s_nop 0
	v_pk_fma_f32 v[48:49], v[22:23], v[32:33], v[42:43] op_sel_hi:[1,0,1]
	v_pk_add_f32 v[22:23], v[24:25], v[50:51]
	v_pk_add_f32 v[24:25], v[24:25], v[50:51] neg_lo:[0,1] neg_hi:[0,1]
	s_nop 0
	v_pk_mul_f32 v[42:43], v[24:25], v[38:39] op_sel:[1,0] op_sel_hi:[0,0] neg_lo:[1,1] neg_hi:[0,1]
	s_nop 0
	v_pk_fma_f32 v[52:53], v[24:25], v[34:35], v[42:43] op_sel_hi:[1,0,1]
	s_waitcnt lgkmcnt(5)
	v_pk_add_f32 v[24:25], v[26:27], v[54:55]
	v_pk_add_f32 v[26:27], v[26:27], v[54:55] neg_lo:[0,1] neg_hi:[0,1]
	s_nop 0
	v_pk_mul_f32 v[42:43], v[26:27], v[10:11] op_sel:[1,0] op_sel_hi:[0,0] neg_lo:[1,1] neg_hi:[0,1]
	s_nop 0
	v_pk_fma_f32 v[54:55], v[26:27], v[10:11], v[42:43] op_sel_hi:[1,0,1]
	v_pk_add_f32 v[26:27], v[28:29], v[56:57]
	v_pk_add_f32 v[28:29], v[28:29], v[56:57] neg_lo:[0,1] neg_hi:[0,1]
	s_nop 0
	v_pk_mul_f32 v[42:43], v[28:29], v[38:39] op_sel_hi:[1,0]
	s_nop 0
	v_pk_fma_f32 v[56:57], v[28:29], v[34:35], v[42:43] op_sel:[1,0,0] op_sel_hi:[0,0,1] neg_lo:[1,1,0] neg_hi:[0,1,0]
	s_waitcnt lgkmcnt(4)
	v_pk_add_f32 v[42:43], v[58:59], v[92:93] neg_lo:[0,1] neg_hi:[0,1]
	v_pk_add_f32 v[28:29], v[58:59], v[92:93]
	v_pk_mul_f32 v[50:51], v[42:43], v[36:37] op_sel_hi:[1,0]
	s_nop 0
	v_pk_fma_f32 v[58:59], v[42:43], v[32:33], v[50:51] op_sel:[1,0,0] op_sel_hi:[0,0,1] neg_lo:[1,1,0] neg_hi:[0,1,0]
	v_pk_add_f32 v[50:51], v[60:61], v[94:95] neg_lo:[0,1] neg_hi:[0,1]
	v_pk_add_f32 v[42:43], v[60:61], v[94:95]
	v_pk_mul_f32 v[60:61], v[50:51], v[46:47] op_sel_hi:[1,0]
	v_xor_b32_e32 v92, 0x80000000, v51
	v_mov_b32_e32 v93, v50
	s_waitcnt lgkmcnt(3)
	v_pk_add_f32 v[50:51], v[76:77], v[96:97]
	v_pk_add_f32 v[76:77], v[76:77], v[96:97] neg_lo:[0,1] neg_hi:[0,1]
	v_pk_fma_f32 v[60:61], v[92:93], v[30:31], v[60:61] op_sel_hi:[1,0,1] neg_lo:[0,1,0] neg_hi:[0,1,0]
	v_xor_b32_e32 v93, 0x80000000, v76
	v_mov_b32_e32 v92, v77
	v_pk_add_f32 v[76:77], v[78:79], v[98:99]
	v_pk_add_f32 v[78:79], v[78:79], v[98:99] neg_lo:[0,1] neg_hi:[0,1]
	s_nop 0
	v_pk_mul_f32 v[94:95], v[78:79], v[46:47] op_sel_hi:[1,0] neg_lo:[0,1] neg_hi:[0,1]
	s_nop 0
	v_pk_fma_f32 v[78:79], v[78:79], v[30:31], v[94:95] op_sel:[1,0,0] op_sel_hi:[0,0,1] neg_lo:[1,1,0] neg_hi:[0,1,0]
	s_waitcnt lgkmcnt(2)
	v_pk_add_f32 v[94:95], v[80:81], v[100:101]
	v_pk_add_f32 v[80:81], v[80:81], v[100:101] neg_lo:[0,1] neg_hi:[0,1]
	s_nop 0
	v_pk_mul_f32 v[96:97], v[80:81], v[36:37] op_sel_hi:[1,0] neg_lo:[0,1] neg_hi:[0,1]
	s_nop 0
	v_pk_fma_f32 v[80:81], v[80:81], v[32:33], v[96:97] op_sel:[1,0,0] op_sel_hi:[0,0,1] neg_lo:[1,1,0] neg_hi:[0,1,0]
	v_pk_add_f32 v[96:97], v[82:83], v[102:103]
	v_pk_add_f32 v[82:83], v[82:83], v[102:103] neg_lo:[0,1] neg_hi:[0,1]
	s_nop 0
	v_pk_mul_f32 v[98:99], v[82:83], v[38:39] op_sel_hi:[1,0] neg_lo:[0,1] neg_hi:[0,1]
	s_nop 0
	v_pk_fma_f32 v[82:83], v[82:83], v[34:35], v[98:99] op_sel:[1,0,0] op_sel_hi:[0,0,1] neg_lo:[1,1,0] neg_hi:[0,1,0]
	s_waitcnt lgkmcnt(1)
	v_pk_add_f32 v[98:99], v[84:85], v[104:105]
	v_pk_add_f32 v[84:85], v[84:85], v[104:105] neg_lo:[0,1] neg_hi:[0,1]
	s_nop 0
	v_pk_mul_f32 v[100:101], v[84:85], v[10:11] op_sel:[1,0] op_sel_hi:[0,0] neg_lo:[1,1] neg_hi:[0,1]
	s_nop 0
	v_pk_fma_f32 v[84:85], v[84:85], v[10:11], v[100:101] op_sel_hi:[1,0,1] neg_lo:[0,1,0] neg_hi:[0,1,0]
	v_pk_add_f32 v[100:101], v[86:87], v[106:107]
	v_pk_add_f32 v[86:87], v[86:87], v[106:107] neg_lo:[0,1] neg_hi:[0,1]
	s_nop 0
	v_pk_mul_f32 v[38:39], v[86:87], v[38:39] op_sel:[1,0] op_sel_hi:[0,0] neg_lo:[1,1] neg_hi:[0,1]
	s_nop 0
	v_pk_fma_f32 v[86:87], v[86:87], v[34:35], v[38:39] op_sel_hi:[1,0,1] neg_lo:[0,1,0] neg_hi:[0,1,0]
	s_waitcnt lgkmcnt(0)
	v_pk_add_f32 v[38:39], v[88:89], v[108:109] neg_lo:[0,1] neg_hi:[0,1]
	v_pk_add_f32 v[34:35], v[88:89], v[108:109]
	v_pk_mul_f32 v[88:89], v[38:39], v[36:37] op_sel:[1,0] op_sel_hi:[0,0] neg_lo:[1,1] neg_hi:[0,1]
	s_nop 0
	v_pk_fma_f32 v[88:89], v[38:39], v[32:33], v[88:89] op_sel_hi:[1,0,1] neg_lo:[0,1,0] neg_hi:[0,1,0]
	v_pk_add_f32 v[38:39], v[90:91], v[110:111]
	v_pk_add_f32 v[90:91], v[90:91], v[110:111] neg_lo:[0,1] neg_hi:[0,1]
	s_nop 0
	v_pk_mul_f32 v[46:47], v[90:91], v[46:47] op_sel:[1,0] op_sel_hi:[0,0] neg_lo:[1,1] neg_hi:[0,1]
	s_nop 0
	v_pk_fma_f32 v[90:91], v[90:91], v[30:31], v[46:47] op_sel_hi:[1,0,1] neg_lo:[0,1,0] neg_hi:[0,1,0]
	v_pk_add_f32 v[46:47], v[18:19], v[76:77]
	v_pk_add_f32 v[18:19], v[18:19], v[76:77] neg_lo:[0,1] neg_hi:[0,1]
	v_pk_add_f32 v[30:31], v[112:113], v[50:51]
	v_pk_mul_f32 v[76:77], v[18:19], v[36:37] op_sel:[1,0] op_sel_hi:[0,0] neg_lo:[1,1] neg_hi:[0,1]
	v_pk_add_f32 v[50:51], v[112:113], v[50:51] neg_lo:[0,1] neg_hi:[0,1]
	v_pk_fma_f32 v[76:77], v[18:19], v[32:33], v[76:77] op_sel_hi:[1,0,1]
	v_pk_add_f32 v[18:19], v[20:21], v[94:95]
	v_pk_add_f32 v[20:21], v[20:21], v[94:95] neg_lo:[0,1] neg_hi:[0,1]
	s_nop 0
	v_pk_mul_f32 v[94:95], v[20:21], v[10:11] op_sel:[1,0] op_sel_hi:[0,0] neg_lo:[1,1] neg_hi:[0,1]
	s_nop 0
	v_pk_fma_f32 v[20:21], v[20:21], v[10:11], v[94:95] op_sel_hi:[1,0,1]
	v_pk_add_f32 v[94:95], v[22:23], v[96:97]
	v_pk_add_f32 v[22:23], v[22:23], v[96:97] neg_lo:[0,1] neg_hi:[0,1]
	s_nop 0
	v_pk_mul_f32 v[96:97], v[22:23], v[36:37] op_sel_hi:[1,0]
	v_xor_b32_e32 v102, 0x80000000, v23
	v_mov_b32_e32 v103, v22
	v_pk_add_f32 v[22:23], v[24:25], v[98:99]
	v_pk_add_f32 v[24:25], v[24:25], v[98:99] neg_lo:[0,1] neg_hi:[0,1]
	v_pk_fma_f32 v[96:97], v[102:103], v[32:33], v[96:97] op_sel_hi:[1,0,1] neg_lo:[0,1,0] neg_hi:[0,1,0]
	v_xor_b32_e32 v99, 0x80000000, v24
	v_mov_b32_e32 v98, v25
	v_pk_add_f32 v[24:25], v[26:27], v[100:101]
	v_pk_add_f32 v[26:27], v[26:27], v[100:101] neg_lo:[0,1] neg_hi:[0,1]
	s_nop 0
	v_pk_mul_f32 v[100:101], v[26:27], v[36:37] op_sel_hi:[1,0] neg_lo:[0,1] neg_hi:[0,1]
	v_xor_b32_e32 v102, 0x80000000, v27
	v_mov_b32_e32 v103, v26
	v_pk_add_f32 v[26:27], v[28:29], v[34:35]
	v_pk_add_f32 v[28:29], v[28:29], v[34:35] neg_lo:[0,1] neg_hi:[0,1]
	v_pk_fma_f32 v[100:101], v[102:103], v[32:33], v[100:101] op_sel_hi:[1,0,1] neg_lo:[0,1,0] neg_hi:[0,1,0]
	v_pk_mul_f32 v[34:35], v[28:29], v[10:11] op_sel:[1,0] op_sel_hi:[0,0] neg_lo:[1,1] neg_hi:[0,1]
	v_pk_add_f32 v[102:103], v[30:31], v[22:23] neg_lo:[0,1] neg_hi:[0,1]
	v_pk_fma_f32 v[28:29], v[28:29], v[10:11], v[34:35] op_sel_hi:[1,0,1] neg_lo:[0,1,0] neg_hi:[0,1,0]
	v_pk_add_f32 v[34:35], v[42:43], v[38:39]
	v_pk_add_f32 v[38:39], v[42:43], v[38:39] neg_lo:[0,1] neg_hi:[0,1]
	s_nop 0
	v_pk_mul_f32 v[42:43], v[38:39], v[36:37] op_sel:[1,0] op_sel_hi:[0,0] neg_lo:[1,1] neg_hi:[0,1]
	s_nop 0
	v_pk_fma_f32 v[42:43], v[38:39], v[32:33], v[42:43] op_sel_hi:[1,0,1] neg_lo:[0,1,0] neg_hi:[0,1,0]
	v_pk_add_f32 v[38:39], v[30:31], v[22:23]
	v_pk_add_f32 v[22:23], v[46:47], v[24:25]
	v_pk_add_f32 v[24:25], v[46:47], v[24:25] neg_lo:[0,1] neg_hi:[0,1]
	s_nop 0
	v_pk_mul_f32 v[30:31], v[24:25], v[10:11] op_sel:[1,0] op_sel_hi:[0,0] neg_lo:[1,1] neg_hi:[0,1]
	s_nop 0
	v_pk_fma_f32 v[24:25], v[24:25], v[10:11], v[30:31] op_sel_hi:[1,0,1]
	v_pk_add_f32 v[30:31], v[18:19], v[26:27]
	v_pk_add_f32 v[18:19], v[18:19], v[26:27] neg_lo:[0,1] neg_hi:[0,1]
	s_nop 0
	v_xor_b32_e32 v27, 0x80000000, v18
	v_mov_b32_e32 v26, v19
	v_pk_add_f32 v[18:19], v[94:95], v[34:35]
	v_pk_add_f32 v[34:35], v[94:95], v[34:35] neg_lo:[0,1] neg_hi:[0,1]
	s_nop 0
	v_pk_mul_f32 v[46:47], v[34:35], v[10:11] op_sel:[1,0] op_sel_hi:[0,0] neg_lo:[1,1] neg_hi:[0,1]
	s_nop 0
	v_pk_fma_f32 v[34:35], v[34:35], v[10:11], v[46:47] op_sel_hi:[1,0,1] neg_lo:[0,1,0] neg_hi:[0,1,0]
	v_pk_add_f32 v[46:47], v[38:39], v[30:31]
	v_pk_add_f32 v[38:39], v[38:39], v[30:31] neg_lo:[0,1] neg_hi:[0,1]
	v_pk_add_f32 v[30:31], v[22:23], v[18:19]
	v_pk_add_f32 v[18:19], v[22:23], v[18:19] neg_lo:[0,1] neg_hi:[0,1]
	v_pk_add_f32 v[94:95], v[46:47], v[30:31]
	v_xor_b32_e32 v23, 0x80000000, v18
	v_mov_b32_e32 v22, v19
	v_pk_add_f32 v[18:19], v[102:103], v[26:27]
	v_pk_add_f32 v[102:103], v[102:103], v[26:27] neg_lo:[0,1] neg_hi:[0,1]
	v_pk_add_f32 v[26:27], v[24:25], v[34:35]
	v_pk_add_f32 v[24:25], v[24:25], v[34:35] neg_lo:[0,1] neg_hi:[0,1]
	v_pk_add_f32 v[30:31], v[46:47], v[30:31] neg_lo:[0,1] neg_hi:[0,1]
	v_xor_b32_e32 v35, 0x80000000, v24
	v_mov_b32_e32 v34, v25
	v_pk_add_f32 v[24:25], v[50:51], v[98:99]
	v_pk_add_f32 v[98:99], v[50:51], v[98:99] neg_lo:[0,1] neg_hi:[0,1]
	v_pk_add_f32 v[50:51], v[76:77], v[100:101] neg_lo:[0,1] neg_hi:[0,1]
	v_pk_add_f32 v[46:47], v[38:39], v[22:23]
	v_pk_add_f32 v[22:23], v[38:39], v[22:23] neg_lo:[0,1] neg_hi:[0,1]
	v_pk_add_f32 v[104:105], v[18:19], v[26:27]
	v_pk_add_f32 v[26:27], v[18:19], v[26:27] neg_lo:[0,1] neg_hi:[0,1]
	v_pk_add_f32 v[38:39], v[102:103], v[34:35]
	v_pk_add_f32 v[18:19], v[102:103], v[34:35] neg_lo:[0,1] neg_hi:[0,1]
	v_pk_add_f32 v[34:35], v[76:77], v[100:101]
	v_pk_mul_f32 v[76:77], v[10:11], v[50:51] op_sel:[0,1] op_sel_hi:[0,0] neg_lo:[1,1] neg_hi:[1,0]
	v_pk_fma_f32 v[76:77], v[10:11], v[50:51], v[76:77] op_sel_hi:[0,1,1]
	v_pk_add_f32 v[50:51], v[20:21], v[28:29]
	v_pk_add_f32 v[20:21], v[20:21], v[28:29] neg_lo:[0,1] neg_hi:[0,1]
	s_nop 0
	v_xor_b32_e32 v29, 0x80000000, v20
	v_mov_b32_e32 v28, v21
	v_pk_add_f32 v[20:21], v[96:97], v[42:43]
	v_pk_add_f32 v[42:43], v[96:97], v[42:43] neg_lo:[0,1] neg_hi:[0,1]
	s_nop 0
	v_pk_mul_f32 v[96:97], v[10:11], v[42:43] op_sel:[0,1] op_sel_hi:[0,0] neg_lo:[1,1] neg_hi:[1,0]
	v_pk_fma_f32 v[42:43], v[10:11], v[42:43], v[96:97] op_sel_hi:[0,1,1] neg_lo:[1,0,0] neg_hi:[1,0,0]
	v_pk_add_f32 v[96:97], v[24:25], v[50:51]
	v_pk_add_f32 v[24:25], v[24:25], v[50:51] neg_lo:[0,1] neg_hi:[0,1]
	v_pk_add_f32 v[50:51], v[34:35], v[20:21]
	v_pk_add_f32 v[20:21], v[34:35], v[20:21] neg_lo:[0,1] neg_hi:[0,1]
	v_pk_add_f32 v[102:103], v[96:97], v[50:51]
	v_xor_b32_e32 v101, 0x80000000, v20
	v_mov_b32_e32 v100, v21
	v_pk_add_f32 v[34:35], v[96:97], v[50:51] neg_lo:[0,1] neg_hi:[0,1]
	v_pk_add_f32 v[20:21], v[98:99], v[28:29]
	v_pk_add_f32 v[96:97], v[98:99], v[28:29] neg_lo:[0,1] neg_hi:[0,1]
	v_pk_add_f32 v[28:29], v[76:77], v[42:43]
	v_pk_add_f32 v[42:43], v[76:77], v[42:43] neg_lo:[0,1] neg_hi:[0,1]
	v_pk_add_f32 v[98:99], v[20:21], v[28:29]
	v_xor_b32_e32 v77, 0x80000000, v42
	v_mov_b32_e32 v76, v43
	v_pk_add_f32 v[28:29], v[20:21], v[28:29] neg_lo:[0,1] neg_hi:[0,1]
	v_pk_add_f32 v[42:43], v[96:97], v[76:77]
	v_pk_add_f32 v[20:21], v[96:97], v[76:77] neg_lo:[0,1] neg_hi:[0,1]
	v_pk_add_f32 v[76:77], v[40:41], v[92:93]
	v_pk_add_f32 v[92:93], v[40:41], v[92:93] neg_lo:[0,1] neg_hi:[0,1]
	v_pk_add_f32 v[40:41], v[44:45], v[78:79]
	v_pk_add_f32 v[44:45], v[44:45], v[78:79] neg_lo:[0,1] neg_hi:[0,1]
	v_pk_add_f32 v[50:51], v[24:25], v[100:101]
	v_pk_mul_f32 v[78:79], v[36:37], v[44:45] op_sel:[0,1] op_sel_hi:[0,0] neg_lo:[1,1] neg_hi:[1,0]
	v_pk_fma_f32 v[44:45], v[32:33], v[44:45], v[78:79] op_sel_hi:[0,1,1]
	v_pk_add_f32 v[78:79], v[48:49], v[80:81]
	v_pk_add_f32 v[48:49], v[48:49], v[80:81] neg_lo:[0,1] neg_hi:[0,1]
	v_pk_add_f32 v[24:25], v[24:25], v[100:101] neg_lo:[0,1] neg_hi:[0,1]
	v_pk_mul_f32 v[80:81], v[10:11], v[48:49] op_sel:[0,1] op_sel_hi:[0,0] neg_lo:[1,1] neg_hi:[1,0]
	v_pk_fma_f32 v[80:81], v[10:11], v[48:49], v[80:81] op_sel_hi:[0,1,1]
	v_pk_add_f32 v[48:49], v[52:53], v[82:83]
	v_pk_add_f32 v[52:53], v[52:53], v[82:83] neg_lo:[0,1] neg_hi:[0,1]
	s_nop 0
	v_pk_mul_f32 v[82:83], v[32:33], v[52:53] op_sel:[0,1] op_sel_hi:[0,0] neg_lo:[1,1] neg_hi:[1,0]
	v_pk_fma_f32 v[52:53], v[36:37], v[52:53], v[82:83] op_sel_hi:[0,1,1]
	v_pk_add_f32 v[82:83], v[54:55], v[84:85]
	v_pk_add_f32 v[54:55], v[54:55], v[84:85] neg_lo:[0,1] neg_hi:[0,1]
	s_nop 0
	v_xor_b32_e32 v85, 0x80000000, v54
	v_mov_b32_e32 v84, v55
	v_pk_add_f32 v[54:55], v[56:57], v[86:87]
	v_pk_add_f32 v[56:57], v[56:57], v[86:87] neg_lo:[0,1] neg_hi:[0,1]
	s_nop 0
	v_pk_mul_f32 v[86:87], v[32:33], v[56:57] op_sel:[0,1] op_sel_hi:[0,0] neg_lo:[1,1] neg_hi:[1,0]
	v_pk_fma_f32 v[56:57], v[36:37], v[56:57], v[86:87] op_sel_hi:[0,1,1] neg_lo:[1,0,0] neg_hi:[1,0,0]
	v_pk_add_f32 v[86:87], v[58:59], v[88:89]
	v_pk_add_f32 v[58:59], v[58:59], v[88:89] neg_lo:[0,1] neg_hi:[0,1]
	s_nop 0
	v_pk_mul_f32 v[88:89], v[10:11], v[58:59] op_sel:[0,1] op_sel_hi:[0,0] neg_lo:[1,1] neg_hi:[1,0]
	v_pk_fma_f32 v[58:59], v[10:11], v[58:59], v[88:89] op_sel_hi:[0,1,1] neg_lo:[1,0,0] neg_hi:[1,0,0]
	v_pk_add_f32 v[88:89], v[60:61], v[90:91]
	v_pk_add_f32 v[60:61], v[60:61], v[90:91] neg_lo:[0,1] neg_hi:[0,1]
	s_nop 0
	v_pk_mul_f32 v[36:37], v[36:37], v[60:61] op_sel:[0,1] op_sel_hi:[0,0] neg_lo:[1,1] neg_hi:[1,0]
	v_pk_fma_f32 v[36:37], v[32:33], v[60:61], v[36:37] op_sel_hi:[0,1,1] neg_lo:[1,0,0] neg_hi:[1,0,0]
	v_pk_add_f32 v[32:33], v[76:77], v[82:83]
	v_pk_add_f32 v[60:61], v[76:77], v[82:83] neg_lo:[0,1] neg_hi:[0,1]
	v_pk_add_f32 v[76:77], v[54:55], v[40:41]
	v_pk_add_f32 v[40:41], v[40:41], v[54:55] neg_lo:[0,1] neg_hi:[0,1]
	s_nop 0
	v_pk_mul_f32 v[54:55], v[10:11], v[40:41] op_sel:[0,1] op_sel_hi:[0,0] neg_lo:[1,1] neg_hi:[1,0]
	v_pk_fma_f32 v[54:55], v[10:11], v[40:41], v[54:55] op_sel_hi:[0,1,1]
	v_pk_add_f32 v[40:41], v[78:79], v[86:87]
	v_pk_add_f32 v[78:79], v[78:79], v[86:87] neg_lo:[0,1] neg_hi:[0,1]
	s_nop 0
	v_xor_b32_e32 v83, 0x80000000, v78
	v_mov_b32_e32 v82, v79
	v_pk_add_f32 v[78:79], v[48:49], v[88:89]
	v_pk_add_f32 v[48:49], v[48:49], v[88:89] neg_lo:[0,1] neg_hi:[0,1]
	v_pk_add_f32 v[88:89], v[76:77], v[78:79]
	v_pk_mul_f32 v[86:87], v[10:11], v[48:49] op_sel:[0,1] op_sel_hi:[0,0] neg_lo:[1,1] neg_hi:[1,0]
	v_pk_fma_f32 v[48:49], v[10:11], v[48:49], v[86:87] op_sel_hi:[0,1,1] neg_lo:[1,0,0] neg_hi:[1,0,0]
	v_pk_add_f32 v[86:87], v[32:33], v[40:41]
	v_pk_add_f32 v[32:33], v[32:33], v[40:41] neg_lo:[0,1] neg_hi:[0,1]
	v_pk_add_f32 v[40:41], v[76:77], v[78:79] neg_lo:[0,1] neg_hi:[0,1]
	v_pk_add_f32 v[78:79], v[86:87], v[88:89] neg_lo:[0,1] neg_hi:[0,1]
	v_pk_add_f32 v[90:91], v[32:33], v[40:41] op_sel:[0,1] op_sel_hi:[1,0] neg_hi:[0,1]
	v_pk_add_f32 v[40:41], v[32:33], v[40:41] op_sel:[0,1] op_sel_hi:[1,0] neg_lo:[0,1]
	v_pk_add_f32 v[76:77], v[54:55], v[48:49]
	v_pk_add_f32 v[48:49], v[54:55], v[48:49] neg_lo:[0,1] neg_hi:[0,1]
	v_pk_add_f32 v[32:33], v[60:61], v[82:83]
	v_pk_add_f32 v[60:61], v[60:61], v[82:83] neg_lo:[0,1] neg_hi:[0,1]
	v_xor_b32_e32 v55, 0x80000000, v48
	v_mov_b32_e32 v54, v49
	v_pk_add_f32 v[82:83], v[32:33], v[76:77]
	v_pk_add_f32 v[48:49], v[32:33], v[76:77] neg_lo:[0,1] neg_hi:[0,1]
	v_pk_add_f32 v[76:77], v[60:61], v[54:55]
	v_pk_add_f32 v[32:33], v[60:61], v[54:55] neg_lo:[0,1] neg_hi:[0,1]
	v_pk_add_f32 v[54:55], v[92:93], v[84:85]
	v_pk_add_f32 v[60:61], v[92:93], v[84:85] neg_lo:[0,1] neg_hi:[0,1]
	v_pk_add_f32 v[84:85], v[56:57], v[44:45]
	v_pk_add_f32 v[44:45], v[44:45], v[56:57] neg_lo:[0,1] neg_hi:[0,1]
	v_pk_add_f32 v[86:87], v[86:87], v[88:89]
	v_pk_mul_f32 v[56:57], v[10:11], v[44:45] op_sel:[0,1] op_sel_hi:[0,0] neg_lo:[1,1] neg_hi:[1,0]
	v_pk_fma_f32 v[56:57], v[10:11], v[44:45], v[56:57] op_sel_hi:[0,1,1]
	v_pk_add_f32 v[44:45], v[80:81], v[58:59]
	v_pk_add_f32 v[58:59], v[80:81], v[58:59] neg_lo:[0,1] neg_hi:[0,1]
	s_nop 0
	v_xor_b32_e32 v81, 0x80000000, v58
	v_mov_b32_e32 v80, v59
	v_pk_add_f32 v[58:59], v[52:53], v[36:37]
	v_pk_add_f32 v[36:37], v[52:53], v[36:37] neg_lo:[0,1] neg_hi:[0,1]
	s_nop 0
	v_pk_mul_f32 v[52:53], v[10:11], v[36:37] op_sel:[0,1] op_sel_hi:[0,0] neg_lo:[1,1] neg_hi:[1,0]
	v_pk_fma_f32 v[36:37], v[10:11], v[36:37], v[52:53] op_sel_hi:[0,1,1] neg_lo:[1,0,0] neg_hi:[1,0,0]
	v_pk_add_f32 v[52:53], v[54:55], v[44:45]
	v_pk_add_f32 v[44:45], v[54:55], v[44:45] neg_lo:[0,1] neg_hi:[0,1]
	v_pk_add_f32 v[54:55], v[84:85], v[58:59]
	v_pk_add_f32 v[58:59], v[84:85], v[58:59] neg_lo:[0,1] neg_hi:[0,1]
	s_nop 0
	v_xor_b32_e32 v85, 0x80000000, v58
	v_mov_b32_e32 v84, v59
	v_pk_add_f32 v[58:59], v[52:53], v[54:55]
	v_pk_add_f32 v[52:53], v[52:53], v[54:55] neg_lo:[0,1] neg_hi:[0,1]
	v_pk_add_f32 v[54:55], v[44:45], v[84:85]
	v_pk_add_f32 v[44:45], v[44:45], v[84:85] neg_lo:[0,1] neg_hi:[0,1]
	v_pk_add_f32 v[84:85], v[60:61], v[80:81]
	v_pk_add_f32 v[60:61], v[60:61], v[80:81] neg_lo:[0,1] neg_hi:[0,1]
	v_pk_add_f32 v[80:81], v[56:57], v[36:37]
	v_pk_add_f32 v[36:37], v[56:57], v[36:37] neg_lo:[0,1] neg_hi:[0,1]
	v_pk_add_f32 v[92:93], v[84:85], v[80:81]
	v_pk_add_f32 v[80:81], v[84:85], v[80:81] neg_lo:[0,1] neg_hi:[0,1]
	v_pk_add_f32 v[84:85], v[60:61], v[36:37] op_sel:[0,1] op_sel_hi:[1,0] neg_hi:[0,1]
	v_pk_add_f32 v[36:37], v[60:61], v[36:37] op_sel:[0,1] op_sel_hi:[1,0] neg_lo:[0,1]
	v_pk_fma_f32 v[60:61], v[16:17], s[92:93], v[16:17] op_sel:[1,0,0] op_sel_hi:[0,1,1]
	v_pk_mul_f32 v[56:57], v[94:95], s[14:15] op_sel:[1,0] neg_lo:[1,0]
	v_pk_mul_f32 v[88:89], v[60:61], v[86:87] op_sel:[1,1] op_sel_hi:[0,1] neg_lo:[0,1]
	v_pk_fma_f32 v[56:57], v[94:95], s[42:43], v[56:57] op_sel_hi:[0,1,1]
	v_pk_fma_f32 v[86:87], v[60:61], v[86:87], v[88:89] op_sel_hi:[1,0,1]
	ds_write2_b64 v75, v[56:57], v[86:87] offset1:16
	v_pk_mul_f32 v[56:57], v[16:17], v[60:61] op_sel:[1,1] op_sel_hi:[0,1] neg_lo:[0,1]
	v_pk_fma_f32 v[56:57], v[16:17], v[60:61], v[56:57] op_sel_hi:[1,0,1]
	s_nop 0
	v_pk_mul_f32 v[60:61], v[56:57], v[102:103] op_sel:[1,1] op_sel_hi:[0,1] neg_lo:[0,1]
	v_pk_mul_f32 v[86:87], v[16:17], v[56:57] op_sel:[1,1] op_sel_hi:[0,1] neg_lo:[0,1]
	v_pk_fma_f32 v[60:61], v[56:57], v[102:103], v[60:61] op_sel_hi:[1,0,1]
	v_pk_fma_f32 v[56:57], v[16:17], v[56:57], v[86:87] op_sel_hi:[1,0,1]
	s_nop 0
	v_pk_mul_f32 v[86:87], v[56:57], v[58:59] op_sel:[1,1] op_sel_hi:[0,1] neg_lo:[0,1]
	v_pk_fma_f32 v[58:59], v[56:57], v[58:59], v[86:87] op_sel_hi:[1,0,1]
	ds_write2_b64 v74, v[60:61], v[58:59] offset0:32 offset1:48
	v_pk_mul_f32 v[58:59], v[16:17], v[56:57] op_sel:[1,1] op_sel_hi:[0,1] neg_lo:[0,1]
	v_pk_fma_f32 v[56:57], v[16:17], v[56:57], v[58:59] op_sel_hi:[1,0,1]
	s_nop 0
	v_pk_mul_f32 v[58:59], v[56:57], v[104:105] op_sel:[1,1] op_sel_hi:[0,1] neg_lo:[0,1]
	v_pk_mul_f32 v[60:61], v[16:17], v[56:57] op_sel:[1,1] op_sel_hi:[0,1] neg_lo:[0,1]
	v_pk_fma_f32 v[58:59], v[56:57], v[104:105], v[58:59] op_sel_hi:[1,0,1]
	v_pk_fma_f32 v[56:57], v[16:17], v[56:57], v[60:61] op_sel_hi:[1,0,1]
	s_nop 0
	v_pk_mul_f32 v[60:61], v[56:57], v[82:83] op_sel:[1,1] op_sel_hi:[0,1] neg_lo:[0,1]
	v_pk_fma_f32 v[60:61], v[56:57], v[82:83], v[60:61] op_sel_hi:[1,0,1]
	ds_write2_b64 v73, v[58:59], v[60:61] offset0:64 offset1:80
	v_pk_mul_f32 v[58:59], v[16:17], v[56:57] op_sel:[1,1] op_sel_hi:[0,1] neg_lo:[0,1]
	v_pk_fma_f32 v[56:57], v[16:17], v[56:57], v[58:59] op_sel_hi:[1,0,1]
	s_nop 0
	v_pk_mul_f32 v[58:59], v[56:57], v[98:99] op_sel:[1,1] op_sel_hi:[0,1] neg_lo:[0,1]
	v_pk_mul_f32 v[60:61], v[16:17], v[56:57] op_sel:[1,1] op_sel_hi:[0,1] neg_lo:[0,1]
	v_pk_fma_f32 v[58:59], v[56:57], v[98:99], v[58:59] op_sel_hi:[1,0,1]
	v_pk_fma_f32 v[56:57], v[16:17], v[56:57], v[60:61] op_sel_hi:[1,0,1]
	s_nop 0
	v_pk_mul_f32 v[60:61], v[56:57], v[92:93] op_sel:[1,1] op_sel_hi:[0,1] neg_lo:[0,1]
	v_pk_fma_f32 v[60:61], v[56:57], v[92:93], v[60:61] op_sel_hi:[1,0,1]
	ds_write2_b64 v72, v[58:59], v[60:61] offset0:96 offset1:112
	v_pk_mul_f32 v[58:59], v[16:17], v[56:57] op_sel:[1,1] op_sel_hi:[0,1] neg_lo:[0,1]
	v_pk_fma_f32 v[56:57], v[16:17], v[56:57], v[58:59] op_sel_hi:[1,0,1]
	s_nop 0
	v_pk_mul_f32 v[58:59], v[56:57], v[46:47] op_sel:[1,1] op_sel_hi:[0,1] neg_lo:[0,1]
	v_pk_fma_f32 v[46:47], v[56:57], v[46:47], v[58:59] op_sel_hi:[1,0,1]
	v_pk_mul_f32 v[58:59], v[16:17], v[56:57] op_sel:[1,1] op_sel_hi:[0,1] neg_lo:[0,1]
	v_pk_fma_f32 v[56:57], v[16:17], v[56:57], v[58:59] op_sel_hi:[1,0,1]
	s_nop 0
	v_pk_mul_f32 v[58:59], v[56:57], v[90:91] op_sel:[1,1] op_sel_hi:[0,1] neg_lo:[0,1]
	v_pk_fma_f32 v[58:59], v[56:57], v[90:91], v[58:59] op_sel_hi:[1,0,1]
	ds_write2_b64 v71, v[46:47], v[58:59] offset0:128 offset1:144
	v_pk_mul_f32 v[46:47], v[16:17], v[56:57] op_sel:[1,1] op_sel_hi:[0,1] neg_lo:[0,1]
	v_pk_fma_f32 v[46:47], v[16:17], v[56:57], v[46:47] op_sel_hi:[1,0,1]
	s_nop 0
	v_pk_mul_f32 v[56:57], v[46:47], v[50:51] op_sel:[1,1] op_sel_hi:[0,1] neg_lo:[0,1]
	v_pk_fma_f32 v[50:51], v[46:47], v[50:51], v[56:57] op_sel_hi:[1,0,1]
	v_pk_mul_f32 v[56:57], v[16:17], v[46:47] op_sel:[1,1] op_sel_hi:[0,1] neg_lo:[0,1]
	v_pk_fma_f32 v[46:47], v[16:17], v[46:47], v[56:57] op_sel_hi:[1,0,1]
	s_nop 0
	v_pk_mul_f32 v[56:57], v[46:47], v[54:55] op_sel:[1,1] op_sel_hi:[0,1] neg_lo:[0,1]
	v_pk_fma_f32 v[54:55], v[46:47], v[54:55], v[56:57] op_sel_hi:[1,0,1]
	ds_write2_b64 v70, v[50:51], v[54:55] offset0:160 offset1:176
	v_pk_mul_f32 v[50:51], v[16:17], v[46:47] op_sel:[1,1] op_sel_hi:[0,1] neg_lo:[0,1]
	v_pk_fma_f32 v[46:47], v[16:17], v[46:47], v[50:51] op_sel_hi:[1,0,1]
	s_nop 0
	v_pk_mul_f32 v[50:51], v[38:39], v[46:47] op_sel:[1,1] op_sel_hi:[1,0] neg_lo:[1,0]
	s_nop 0
	v_pk_fma_f32 v[38:39], v[38:39], v[46:47], v[50:51] op_sel_hi:[0,1,1]
	v_pk_mul_f32 v[50:51], v[16:17], v[46:47] op_sel:[1,1] op_sel_hi:[0,1] neg_lo:[0,1]
	v_pk_fma_f32 v[46:47], v[16:17], v[46:47], v[50:51] op_sel_hi:[1,0,1]
	s_nop 0
	v_pk_mul_f32 v[50:51], v[46:47], v[76:77] op_sel:[1,1] op_sel_hi:[0,1] neg_lo:[0,1]
	v_pk_fma_f32 v[50:51], v[46:47], v[76:77], v[50:51] op_sel_hi:[1,0,1]
	ds_write2_b64 v69, v[38:39], v[50:51] offset0:192 offset1:208
	v_pk_mul_f32 v[38:39], v[16:17], v[46:47] op_sel:[1,1] op_sel_hi:[0,1] neg_lo:[0,1]
	v_pk_fma_f32 v[38:39], v[16:17], v[46:47], v[38:39] op_sel_hi:[1,0,1]
	s_nop 0
	v_pk_mul_f32 v[46:47], v[42:43], v[38:39] op_sel:[1,1] op_sel_hi:[1,0] neg_lo:[1,0]
	s_nop 0
	v_pk_fma_f32 v[42:43], v[42:43], v[38:39], v[46:47] op_sel_hi:[0,1,1]
	v_pk_mul_f32 v[46:47], v[16:17], v[38:39] op_sel:[1,1] op_sel_hi:[0,1] neg_lo:[0,1]
	v_pk_fma_f32 v[38:39], v[16:17], v[38:39], v[46:47] op_sel_hi:[1,0,1]
	s_nop 0
	v_pk_mul_f32 v[46:47], v[38:39], v[84:85] op_sel:[1,1] op_sel_hi:[0,1] neg_lo:[0,1]
	v_pk_fma_f32 v[46:47], v[38:39], v[84:85], v[46:47] op_sel_hi:[1,0,1]
	ds_write2_b64 v68, v[42:43], v[46:47] offset0:224 offset1:240
	v_pk_mul_f32 v[42:43], v[16:17], v[38:39] op_sel:[1,1] op_sel_hi:[0,1] neg_lo:[0,1]
	v_pk_fma_f32 v[38:39], v[16:17], v[38:39], v[42:43] op_sel_hi:[1,0,1]
	s_nop 0
	v_pk_mul_f32 v[42:43], v[30:31], v[38:39] op_sel:[1,1] op_sel_hi:[1,0] neg_lo:[1,0]
	s_nop 0
	v_pk_fma_f32 v[30:31], v[30:31], v[38:39], v[42:43] op_sel_hi:[0,1,1]
	v_pk_mul_f32 v[42:43], v[16:17], v[38:39] op_sel:[1,1] op_sel_hi:[0,1] neg_lo:[0,1]
	v_pk_fma_f32 v[38:39], v[16:17], v[38:39], v[42:43] op_sel_hi:[1,0,1]
	s_nop 0
	v_pk_mul_f32 v[42:43], v[78:79], v[38:39] op_sel:[1,1] op_sel_hi:[1,0] neg_lo:[1,0]
	s_nop 0
	v_pk_fma_f32 v[42:43], v[78:79], v[38:39], v[42:43] op_sel_hi:[0,1,1]
	ds_write2_b64 v67, v[30:31], v[42:43] offset1:16
	v_pk_mul_f32 v[30:31], v[16:17], v[38:39] op_sel:[1,1] op_sel_hi:[0,1] neg_lo:[0,1]
	v_pk_fma_f32 v[30:31], v[16:17], v[38:39], v[30:31] op_sel_hi:[1,0,1]
	s_nop 0
	v_pk_mul_f32 v[38:39], v[34:35], v[30:31] op_sel:[1,1] op_sel_hi:[1,0] neg_lo:[1,0]
	s_nop 0
	v_pk_fma_f32 v[34:35], v[34:35], v[30:31], v[38:39] op_sel_hi:[0,1,1]
	v_pk_mul_f32 v[38:39], v[16:17], v[30:31] op_sel:[1,1] op_sel_hi:[0,1] neg_lo:[0,1]
	v_pk_fma_f32 v[30:31], v[16:17], v[30:31], v[38:39] op_sel_hi:[1,0,1]
	s_nop 0
	v_pk_mul_f32 v[38:39], v[52:53], v[30:31] op_sel:[1,1] op_sel_hi:[1,0] neg_lo:[1,0]
	s_nop 0
	v_pk_fma_f32 v[38:39], v[52:53], v[30:31], v[38:39] op_sel_hi:[0,1,1]
	ds_write2_b64 v66, v[34:35], v[38:39] offset0:32 offset1:48
	v_pk_mul_f32 v[34:35], v[16:17], v[30:31] op_sel:[1,1] op_sel_hi:[0,1] neg_lo:[0,1]
	v_pk_fma_f32 v[30:31], v[16:17], v[30:31], v[34:35] op_sel_hi:[1,0,1]
	s_nop 0
	v_pk_mul_f32 v[34:35], v[26:27], v[30:31] op_sel:[1,1] op_sel_hi:[1,0] neg_lo:[1,0]
	s_nop 0
	v_pk_fma_f32 v[26:27], v[26:27], v[30:31], v[34:35] op_sel_hi:[0,1,1]
	v_pk_mul_f32 v[34:35], v[16:17], v[30:31] op_sel:[1,1] op_sel_hi:[0,1] neg_lo:[0,1]
	v_pk_fma_f32 v[30:31], v[16:17], v[30:31], v[34:35] op_sel_hi:[1,0,1]
	s_nop 0
	v_pk_mul_f32 v[34:35], v[48:49], v[30:31] op_sel:[1,1] op_sel_hi:[1,0] neg_lo:[1,0]
	s_nop 0
	v_pk_fma_f32 v[34:35], v[48:49], v[30:31], v[34:35] op_sel_hi:[0,1,1]
	ds_write2_b64 v65, v[26:27], v[34:35] offset0:64 offset1:80
	v_pk_mul_f32 v[26:27], v[16:17], v[30:31] op_sel:[1,1] op_sel_hi:[0,1] neg_lo:[0,1]
	v_pk_fma_f32 v[26:27], v[16:17], v[30:31], v[26:27] op_sel_hi:[1,0,1]
	s_nop 0
	v_pk_mul_f32 v[30:31], v[28:29], v[26:27] op_sel:[1,1] op_sel_hi:[1,0] neg_lo:[1,0]
	s_nop 0
	v_pk_fma_f32 v[28:29], v[28:29], v[26:27], v[30:31] op_sel_hi:[0,1,1]
	v_pk_mul_f32 v[30:31], v[16:17], v[26:27] op_sel:[1,1] op_sel_hi:[0,1] neg_lo:[0,1]
	v_pk_fma_f32 v[26:27], v[16:17], v[26:27], v[30:31] op_sel_hi:[1,0,1]
	s_nop 0
	v_pk_mul_f32 v[30:31], v[80:81], v[26:27] op_sel:[1,1] op_sel_hi:[1,0] neg_lo:[1,0]
	s_nop 0
	v_pk_fma_f32 v[30:31], v[80:81], v[26:27], v[30:31] op_sel_hi:[0,1,1]
	ds_write2_b64 v64, v[28:29], v[30:31] offset0:96 offset1:112
	v_pk_mul_f32 v[28:29], v[16:17], v[26:27] op_sel:[1,1] op_sel_hi:[0,1] neg_lo:[0,1]
	v_pk_fma_f32 v[26:27], v[16:17], v[26:27], v[28:29] op_sel_hi:[1,0,1]
	s_nop 0
	v_pk_mul_f32 v[28:29], v[22:23], v[26:27] op_sel:[1,1] op_sel_hi:[1,0] neg_lo:[1,0]
	s_nop 0
	v_pk_fma_f32 v[22:23], v[22:23], v[26:27], v[28:29] op_sel_hi:[0,1,1]
	v_pk_mul_f32 v[28:29], v[16:17], v[26:27] op_sel:[1,1] op_sel_hi:[0,1] neg_lo:[0,1]
	v_pk_fma_f32 v[26:27], v[16:17], v[26:27], v[28:29] op_sel_hi:[1,0,1]
	s_nop 0
	v_pk_mul_f32 v[28:29], v[40:41], v[26:27] op_sel:[1,1] op_sel_hi:[1,0] neg_lo:[1,0]
	s_nop 0
	v_pk_fma_f32 v[28:29], v[40:41], v[26:27], v[28:29] op_sel_hi:[0,1,1]
	ds_write2_b64 v63, v[22:23], v[28:29] offset0:128 offset1:144
	v_pk_mul_f32 v[22:23], v[16:17], v[26:27] op_sel:[1,1] op_sel_hi:[0,1] neg_lo:[0,1]
	v_pk_fma_f32 v[22:23], v[16:17], v[26:27], v[22:23] op_sel_hi:[1,0,1]
	s_nop 0
	v_pk_mul_f32 v[26:27], v[24:25], v[22:23] op_sel:[1,1] op_sel_hi:[1,0] neg_lo:[1,0]
	s_nop 0
	v_pk_fma_f32 v[24:25], v[24:25], v[22:23], v[26:27] op_sel_hi:[0,1,1]
	v_pk_mul_f32 v[26:27], v[16:17], v[22:23] op_sel:[1,1] op_sel_hi:[0,1] neg_lo:[0,1]
	v_pk_fma_f32 v[22:23], v[16:17], v[22:23], v[26:27] op_sel_hi:[1,0,1]
	s_nop 0
	v_pk_mul_f32 v[26:27], v[44:45], v[22:23] op_sel:[1,1] op_sel_hi:[1,0] neg_lo:[1,0]
	s_nop 0
	v_pk_fma_f32 v[26:27], v[44:45], v[22:23], v[26:27] op_sel_hi:[0,1,1]
	ds_write2_b64 v62, v[24:25], v[26:27] offset0:160 offset1:176
	v_pk_mul_f32 v[24:25], v[16:17], v[22:23] op_sel:[1,1] op_sel_hi:[0,1] neg_lo:[0,1]
	v_pk_fma_f32 v[22:23], v[16:17], v[22:23], v[24:25] op_sel_hi:[1,0,1]
	s_nop 0
	v_pk_mul_f32 v[24:25], v[18:19], v[22:23] op_sel:[1,1] op_sel_hi:[1,0] neg_lo:[1,0]
	s_nop 0
	v_pk_fma_f32 v[18:19], v[18:19], v[22:23], v[24:25] op_sel_hi:[0,1,1]
	v_pk_mul_f32 v[24:25], v[16:17], v[22:23] op_sel:[1,1] op_sel_hi:[0,1] neg_lo:[0,1]
	v_pk_fma_f32 v[22:23], v[16:17], v[22:23], v[24:25] op_sel_hi:[1,0,1]
	s_nop 0
	v_pk_mul_f32 v[24:25], v[32:33], v[22:23] op_sel:[1,1] op_sel_hi:[1,0] neg_lo:[1,0]
	s_nop 0
	v_pk_fma_f32 v[24:25], v[32:33], v[22:23], v[24:25] op_sel_hi:[0,1,1]
	ds_write2_b64 v15, v[18:19], v[24:25] offset0:192 offset1:208
	v_pk_mul_f32 v[18:19], v[16:17], v[22:23] op_sel:[1,1] op_sel_hi:[0,1] neg_lo:[0,1]
	v_pk_fma_f32 v[18:19], v[16:17], v[22:23], v[18:19] op_sel_hi:[1,0,1]
	s_nop 0
	v_pk_mul_f32 v[22:23], v[20:21], v[18:19] op_sel:[1,1] op_sel_hi:[1,0] neg_lo:[1,0]
	s_nop 0
	v_pk_fma_f32 v[20:21], v[20:21], v[18:19], v[22:23] op_sel_hi:[0,1,1]
	v_pk_mul_f32 v[22:23], v[16:17], v[18:19] op_sel:[1,1] op_sel_hi:[0,1] neg_lo:[0,1]
	v_pk_fma_f32 v[16:17], v[16:17], v[18:19], v[22:23] op_sel_hi:[1,0,1]
	s_nop 0
	v_pk_mul_f32 v[18:19], v[36:37], v[16:17] op_sel:[1,1] op_sel_hi:[1,0] neg_lo:[1,0]
	s_nop 0
	v_pk_fma_f32 v[16:17], v[36:37], v[16:17], v[18:19] op_sel_hi:[0,1,1]
	ds_write2_b64 v13, v[20:21], v[16:17] offset0:224 offset1:240
	v_mov_b32_e32 v16, v1
	v_mov_b32_e32 v10, v178
	v_mov_b32_e32 v17, v177
	s_waitcnt lgkmcnt(0)
	s_barrier
	v_lshlrev_b32_e32 v190, 3, v16
	v_add_u32_e32 v190, 0x1000, v190
	global_load_dwordx2 v[196:197], v190, s[48:49] offset:-4096
	global_load_dwordx2 v[198:199], v190, s[48:49]
	v_add_u32_e32 v190, 0x2000, v190
	global_load_dwordx2 v[200:201], v190, s[48:49] offset:-4096
	global_load_dwordx2 v[202:203], v190, s[48:49]
	v_add_u32_e32 v190, 0x2000, v190
	global_load_dwordx2 v[204:205], v190, s[48:49] offset:-4096
	global_load_dwordx2 v[206:207], v190, s[48:49]
	v_add_u32_e32 v190, 0x2000, v190
	global_load_dwordx2 v[208:209], v190, s[48:49] offset:-4096
	global_load_dwordx2 v[210:211], v190, s[48:49]
	v_add_u32_e32 v190, 0x2000, v190
	global_load_dwordx2 v[212:213], v190, s[48:49] offset:-4096
	global_load_dwordx2 v[214:215], v190, s[48:49]
	v_add_u32_e32 v190, 0x2000, v190
	global_load_dwordx2 v[216:217], v190, s[48:49] offset:-4096
	global_load_dwordx2 v[218:219], v190, s[48:49]
	v_add_u32_e32 v190, 0x2000, v190
	global_load_dwordx2 v[220:221], v190, s[48:49] offset:-4096
	global_load_dwordx2 v[222:223], v190, s[48:49]
	v_add_u32_e32 v190, 0x2000, v190
	global_load_dwordx2 v[224:225], v190, s[48:49] offset:-4096
	global_load_dwordx2 v[226:227], v190, s[48:49]
	v_mov_b32_e32 v50, v166
	v_lshlrev_b32_e32 v13, 3, v17
	v_lshlrev_b32_e32 v48, 3, v10
	v_add3_u32 v10, 0, v13, v48
	v_xor_b32_e32 v13, 1, v17
	v_xor_b32_e32 v34, 8, v17
	v_xor_b32_e32 v36, 9, v17
	v_lshlrev_b32_e32 v13, 3, v13
	v_xor_b32_e32 v15, 2, v17
	v_xor_b32_e32 v24, 3, v17
	v_xor_b32_e32 v26, 4, v17
	v_xor_b32_e32 v28, 5, v17
	v_xor_b32_e32 v30, 6, v17
	v_xor_b32_e32 v32, 7, v17
	v_lshlrev_b32_e32 v34, 3, v34
	v_lshlrev_b32_e32 v36, 3, v36
	v_xor_b32_e32 v38, 10, v17
	v_xor_b32_e32 v40, 11, v17
	v_xor_b32_e32 v42, 12, v17
	v_xor_b32_e32 v44, 13, v17
	v_xor_b32_e32 v46, 14, v17
	v_xor_b32_e32 v17, 15, v17
	v_add3_u32 v13, 0, v13, v48
	v_lshlrev_b32_e32 v15, 3, v15
	v_lshlrev_b32_e32 v24, 3, v24
	v_lshlrev_b32_e32 v26, 3, v26
	v_lshlrev_b32_e32 v28, 3, v28
	v_lshlrev_b32_e32 v30, 3, v30
	v_lshlrev_b32_e32 v32, 3, v32
	v_add3_u32 v57, 0, v34, v48
	v_add3_u32 v58, 0, v36, v48
	v_lshlrev_b32_e32 v38, 3, v38
	v_lshlrev_b32_e32 v40, 3, v40
	v_lshlrev_b32_e32 v42, 3, v42
	v_lshlrev_b32_e32 v44, 3, v44
	v_lshlrev_b32_e32 v46, 3, v46
	v_lshlrev_b32_e32 v17, 3, v17
	ds_read_b64 v[18:19], v10
	ds_read_b64 v[20:21], v13
	v_add3_u32 v15, 0, v15, v48
	v_add3_u32 v52, 0, v24, v48
	v_add3_u32 v53, 0, v26, v48
	v_add3_u32 v54, 0, v28, v48
	v_add3_u32 v55, 0, v30, v48
	v_add3_u32 v56, 0, v32, v48
	ds_read_b64 v[34:35], v57
	ds_read_b64 v[36:37], v58
	v_add3_u32 v59, 0, v38, v48
	v_add3_u32 v60, 0, v40, v48
	v_add3_u32 v61, 0, v42, v48
	v_add3_u32 v62, 0, v44, v48
	v_add3_u32 v63, 0, v46, v48
	v_add3_u32 v64, 0, v17, v48
	v_mov_b32_e32 v17, v164
	ds_read_b64 v[22:23], v15
	ds_read_b64 v[24:25], v52
	ds_read_b64 v[26:27], v53
	ds_read_b64 v[28:29], v54
	ds_read_b64 v[30:31], v55
	ds_read_b64 v[32:33], v56
	ds_read_b64 v[38:39], v59
	ds_read_b64 v[40:41], v60
	ds_read_b64 v[42:43], v61
	ds_read_b64 v[44:45], v62
	ds_read_b64 v[46:47], v63
	ds_read_b64 v[48:49], v64
	s_waitcnt lgkmcnt(13)
	v_pk_add_f32 v[70:71], v[18:19], v[34:35]
	v_mov_b32_e32 v17, v165
	v_pk_add_f32 v[18:19], v[18:19], v[34:35] neg_lo:[0,1] neg_hi:[0,1]
	v_mov_b32_e32 v17, v167
	s_waitcnt lgkmcnt(12)
	v_pk_add_f32 v[34:35], v[20:21], v[36:37]
	v_pk_add_f32 v[20:21], v[20:21], v[36:37] neg_lo:[0,1] neg_hi:[0,1]
	v_mov_b32_e32 v66, v168
	v_mov_b32_e32 v17, v169
	v_mov_b32_e32 v68, v170
	s_nop 0
	v_pk_mul_f32 v[36:37], v[20:21], v[68:69] op_sel:[1,0] op_sel_hi:[0,0] neg_lo:[1,1] neg_hi:[0,1]
	v_mov_b32_e32 v17, v171
	v_pk_fma_f32 v[20:21], v[20:21], v[50:51], v[36:37] op_sel_hi:[1,0,1]
	s_waitcnt lgkmcnt(5)
	v_pk_add_f32 v[36:37], v[22:23], v[38:39]
	v_pk_add_f32 v[22:23], v[22:23], v[38:39] neg_lo:[0,1] neg_hi:[0,1]
	s_nop 0
	v_pk_mul_f32 v[38:39], v[22:23], v[66:67] op_sel:[1,0] op_sel_hi:[0,0] neg_lo:[1,1] neg_hi:[0,1]
	v_mov_b32_e32 v17, v172
	v_pk_fma_f32 v[22:23], v[22:23], v[66:67], v[38:39] op_sel_hi:[1,0,1]
	s_waitcnt lgkmcnt(4)
	v_pk_add_f32 v[38:39], v[24:25], v[40:41]
	v_pk_add_f32 v[24:25], v[24:25], v[40:41] neg_lo:[0,1] neg_hi:[0,1]
	s_nop 0
	v_pk_mul_f32 v[40:41], v[24:25], v[68:69] op_sel_hi:[1,0]
	s_nop 0
	v_pk_fma_f32 v[24:25], v[24:25], v[50:51], v[40:41] op_sel:[1,0,0] op_sel_hi:[0,0,1] neg_lo:[1,1,0] neg_hi:[0,1,0]
	s_waitcnt lgkmcnt(3)
	v_pk_add_f32 v[40:41], v[26:27], v[42:43]
	v_pk_add_f32 v[26:27], v[26:27], v[42:43] neg_lo:[0,1] neg_hi:[0,1]
	v_ashrrev_i32_e32 v17, 31, v16
	v_xor_b32_e32 v73, 0x80000000, v26
	v_mov_b32_e32 v72, v27
	s_waitcnt lgkmcnt(2)
	v_pk_add_f32 v[26:27], v[28:29], v[44:45]
	v_pk_add_f32 v[28:29], v[28:29], v[44:45] neg_lo:[0,1] neg_hi:[0,1]
	s_nop 0
	v_pk_mul_f32 v[42:43], v[28:29], v[68:69] op_sel_hi:[1,0] neg_lo:[0,1] neg_hi:[0,1]
	s_nop 0
	v_pk_fma_f32 v[28:29], v[28:29], v[50:51], v[42:43] op_sel:[1,0,0] op_sel_hi:[0,0,1] neg_lo:[1,1,0] neg_hi:[0,1,0]
	s_waitcnt lgkmcnt(1)
	v_pk_add_f32 v[42:43], v[30:31], v[46:47]
	v_pk_add_f32 v[30:31], v[30:31], v[46:47] neg_lo:[0,1] neg_hi:[0,1]
	s_nop 0
	v_pk_mul_f32 v[44:45], v[30:31], v[66:67] op_sel:[1,0] op_sel_hi:[0,0] neg_lo:[1,1] neg_hi:[0,1]
	s_nop 0
	v_pk_fma_f32 v[30:31], v[30:31], v[66:67], v[44:45] op_sel_hi:[1,0,1] neg_lo:[0,1,0] neg_hi:[0,1,0]
	s_waitcnt lgkmcnt(0)
	v_pk_add_f32 v[44:45], v[32:33], v[48:49]
	v_pk_add_f32 v[32:33], v[32:33], v[48:49] neg_lo:[0,1] neg_hi:[0,1]
	v_pk_add_f32 v[48:49], v[34:35], v[26:27]
	v_pk_add_f32 v[26:27], v[34:35], v[26:27] neg_lo:[0,1] neg_hi:[0,1]
	s_nop 0
	v_pk_mul_f32 v[34:35], v[26:27], v[66:67] op_sel:[1,0] op_sel_hi:[0,0] neg_lo:[1,1] neg_hi:[0,1]
	v_pk_fma_f32 v[26:27], v[26:27], v[66:67], v[34:35] op_sel_hi:[1,0,1]
	v_pk_add_f32 v[34:35], v[36:37], v[42:43]
	v_pk_add_f32 v[36:37], v[36:37], v[42:43] neg_lo:[0,1] neg_hi:[0,1]
	v_pk_mul_f32 v[46:47], v[32:33], v[68:69] op_sel:[1,0] op_sel_hi:[0,0] neg_lo:[1,1] neg_hi:[0,1]
	v_xor_b32_e32 v43, 0x80000000, v36
	v_mov_b32_e32 v42, v37
	v_pk_add_f32 v[36:37], v[38:39], v[44:45]
	v_pk_add_f32 v[38:39], v[38:39], v[44:45] neg_lo:[0,1] neg_hi:[0,1]
	v_pk_fma_f32 v[46:47], v[32:33], v[50:51], v[46:47] op_sel_hi:[1,0,1] neg_lo:[0,1,0] neg_hi:[0,1,0]
	v_pk_add_f32 v[32:33], v[70:71], v[40:41]
	v_pk_mul_f32 v[44:45], v[38:39], v[66:67] op_sel:[1,0] op_sel_hi:[0,0] neg_lo:[1,1] neg_hi:[0,1]
	v_pk_add_f32 v[40:41], v[70:71], v[40:41] neg_lo:[0,1] neg_hi:[0,1]
	v_pk_fma_f32 v[38:39], v[38:39], v[66:67], v[44:45] op_sel_hi:[1,0,1] neg_lo:[0,1,0] neg_hi:[0,1,0]
	v_pk_add_f32 v[44:45], v[32:33], v[34:35]
	v_pk_add_f32 v[32:33], v[32:33], v[34:35] neg_lo:[0,1] neg_hi:[0,1]
	v_pk_add_f32 v[34:35], v[48:49], v[36:37]
	v_pk_add_f32 v[36:37], v[48:49], v[36:37] neg_lo:[0,1] neg_hi:[0,1]
	v_pk_add_f32 v[50:51], v[44:45], v[34:35]
	v_xor_b32_e32 v49, 0x80000000, v36
	v_mov_b32_e32 v48, v37
	v_pk_add_f32 v[36:37], v[44:45], v[34:35] neg_lo:[0,1] neg_hi:[0,1]
	v_pk_add_f32 v[68:69], v[32:33], v[48:49]
	v_pk_add_f32 v[44:45], v[32:33], v[48:49] neg_lo:[0,1] neg_hi:[0,1]
	v_pk_add_f32 v[32:33], v[40:41], v[42:43]
	v_pk_add_f32 v[34:35], v[40:41], v[42:43] neg_lo:[0,1] neg_hi:[0,1]
	v_pk_add_f32 v[40:41], v[26:27], v[38:39]
	v_pk_add_f32 v[26:27], v[26:27], v[38:39] neg_lo:[0,1] neg_hi:[0,1]
	v_pk_add_f32 v[42:43], v[32:33], v[40:41] neg_lo:[0,1] neg_hi:[0,1]
	v_xor_b32_e32 v39, 0x80000000, v26
	v_mov_b32_e32 v38, v27
	v_pk_add_f32 v[26:27], v[32:33], v[40:41]
	v_pk_add_f32 v[40:41], v[20:21], v[28:29]
	v_pk_add_f32 v[20:21], v[20:21], v[28:29] neg_lo:[0,1] neg_hi:[0,1]
	v_pk_add_f32 v[32:33], v[34:35], v[38:39]
	v_pk_mul_f32 v[28:29], v[66:67], v[20:21] op_sel:[0,1] op_sel_hi:[0,0] neg_lo:[1,1] neg_hi:[1,0]
	v_pk_fma_f32 v[20:21], v[66:67], v[20:21], v[28:29] op_sel_hi:[0,1,1]
	v_pk_add_f32 v[28:29], v[22:23], v[30:31]
	v_pk_add_f32 v[22:23], v[22:23], v[30:31] neg_lo:[0,1] neg_hi:[0,1]
	v_pk_add_f32 v[38:39], v[34:35], v[38:39] neg_lo:[0,1] neg_hi:[0,1]
	v_xor_b32_e32 v31, 0x80000000, v22
	v_mov_b32_e32 v30, v23
	v_pk_add_f32 v[22:23], v[24:25], v[46:47]
	v_pk_add_f32 v[24:25], v[24:25], v[46:47] neg_lo:[0,1] neg_hi:[0,1]
	v_pk_add_f32 v[34:35], v[18:19], v[72:73]
	v_pk_mul_f32 v[46:47], v[66:67], v[24:25] op_sel:[0,1] op_sel_hi:[0,0] neg_lo:[1,1] neg_hi:[1,0]
	v_pk_fma_f32 v[24:25], v[66:67], v[24:25], v[46:47] op_sel_hi:[0,1,1] neg_lo:[1,0,0] neg_hi:[1,0,0]
	v_pk_add_f32 v[46:47], v[34:35], v[28:29]
	v_pk_add_f32 v[28:29], v[34:35], v[28:29] neg_lo:[0,1] neg_hi:[0,1]
	v_pk_add_f32 v[34:35], v[40:41], v[22:23]
	v_pk_add_f32 v[22:23], v[40:41], v[22:23] neg_lo:[0,1] neg_hi:[0,1]
	v_pk_add_f32 v[18:19], v[18:19], v[72:73] neg_lo:[0,1] neg_hi:[0,1]
	v_pk_add_f32 v[66:67], v[28:29], v[22:23] op_sel:[0,1] op_sel_hi:[1,0] neg_hi:[0,1]
	v_pk_add_f32 v[48:49], v[28:29], v[22:23] op_sel:[0,1] op_sel_hi:[1,0] neg_lo:[0,1]
	v_pk_add_f32 v[28:29], v[18:19], v[30:31]
	v_pk_add_f32 v[18:19], v[18:19], v[30:31] neg_lo:[0,1] neg_hi:[0,1]
	v_pk_add_f32 v[30:31], v[20:21], v[24:25]
	v_pk_add_f32 v[20:21], v[20:21], v[24:25] neg_lo:[0,1] neg_hi:[0,1]
	v_pk_add_f32 v[22:23], v[46:47], v[34:35]
	v_xor_b32_e32 v25, 0x80000000, v20
	v_mov_b32_e32 v24, v21
	v_lshl_add_u64 v[20:21], v[16:17], 3, s[48:49]
	s_waitcnt vmcnt(0)
	v_pk_add_f32 v[40:41], v[46:47], v[34:35] neg_lo:[0,1] neg_hi:[0,1]
	v_pk_add_f32 v[34:35], v[18:19], v[24:25]
	v_pk_add_f32 v[18:19], v[18:19], v[24:25] neg_lo:[0,1] neg_hi:[0,1]
	v_pk_add_f32 v[70:71], v[28:29], v[30:31]
	v_pk_add_f32 v[46:47], v[28:29], v[30:31] neg_lo:[0,1] neg_hi:[0,1]
	v_mov_b32_e32 v17, v164
	s_nop 0
	v_pk_mul_f32 v[24:25], v[50:51], v[196:197] op_sel:[1,1] op_sel_hi:[1,0] neg_lo:[1,0]
	s_nop 0
	v_pk_fma_f32 v[20:21], v[50:51], v[196:197], v[24:25] op_sel_hi:[0,1,1]
	v_add_u32_e32 v24, 0x200, v16
	v_ashrrev_i32_e32 v25, 31, v24
	v_lshl_add_u64 v[24:25], v[24:25], 3, s[48:49]
	s_nop 0
	v_pk_mul_f32 v[28:29], v[198:199], v[22:23] op_sel:[1,1] op_sel_hi:[0,1] neg_lo:[0,1]
	v_pk_fma_f32 v[22:23], v[198:199], v[22:23], v[28:29] op_sel_hi:[1,0,1]
	v_add_u32_e32 v24, 0x400, v16
	v_ashrrev_i32_e32 v25, 31, v24
	v_lshl_add_u64 v[24:25], v[24:25], 3, s[48:49]
	s_nop 0
	v_pk_mul_f32 v[28:29], v[26:27], v[200:201] op_sel:[1,1] op_sel_hi:[1,0] neg_lo:[1,0]
	s_nop 0
	v_pk_fma_f32 v[24:25], v[26:27], v[200:201], v[28:29] op_sel_hi:[0,1,1]
	v_add_u32_e32 v26, 0x600, v16
	v_ashrrev_i32_e32 v27, 31, v26
	v_lshl_add_u64 v[26:27], v[26:27], 3, s[48:49]
	s_nop 0
	v_pk_mul_f32 v[28:29], v[202:203], v[70:71] op_sel:[1,1] op_sel_hi:[0,1] neg_lo:[0,1]
	v_pk_fma_f32 v[26:27], v[202:203], v[70:71], v[28:29] op_sel_hi:[1,0,1]
	v_add_u32_e32 v28, 0x800, v16
	v_ashrrev_i32_e32 v29, 31, v28
	v_lshl_add_u64 v[28:29], v[28:29], 3, s[48:49]
	s_nop 0
	v_pk_mul_f32 v[30:31], v[68:69], v[204:205] op_sel:[1,1] op_sel_hi:[1,0] neg_lo:[1,0]
	s_nop 0
	v_pk_fma_f32 v[28:29], v[68:69], v[204:205], v[30:31] op_sel_hi:[0,1,1]
	v_add_u32_e32 v30, 0xa00, v16
	v_ashrrev_i32_e32 v31, 31, v30
	v_lshl_add_u64 v[30:31], v[30:31], 3, s[48:49]
	v_mov_b32_e32 v68, v170
	s_nop 0
	v_pk_mul_f32 v[50:51], v[206:207], v[66:67] op_sel:[1,1] op_sel_hi:[0,1] neg_lo:[0,1]
	v_pk_fma_f32 v[30:31], v[206:207], v[66:67], v[50:51] op_sel_hi:[1,0,1]
	v_add_u32_e32 v50, 0xc00, v16
	v_ashrrev_i32_e32 v51, 31, v50
	v_lshl_add_u64 v[50:51], v[50:51], 3, s[48:49]
	s_nop 0
	v_pk_mul_f32 v[66:67], v[32:33], v[208:209] op_sel:[1,1] op_sel_hi:[1,0] neg_lo:[1,0]
	s_nop 0
	v_pk_fma_f32 v[32:33], v[32:33], v[208:209], v[66:67] op_sel_hi:[0,1,1]
	v_add_u32_e32 v50, 0xe00, v16
	v_ashrrev_i32_e32 v51, 31, v50
	v_lshl_add_u64 v[50:51], v[50:51], 3, s[48:49]
	s_nop 0
	v_pk_mul_f32 v[66:67], v[210:211], v[34:35] op_sel:[1,1] op_sel_hi:[0,1] neg_lo:[0,1]
	v_pk_fma_f32 v[34:35], v[210:211], v[34:35], v[66:67] op_sel_hi:[1,0,1]
	v_add_u32_e32 v50, 0x1000, v16
	v_ashrrev_i32_e32 v51, 31, v50
	v_lshl_add_u64 v[50:51], v[50:51], 3, s[48:49]
	s_nop 0
	v_pk_mul_f32 v[66:67], v[36:37], v[212:213] op_sel:[1,1] op_sel_hi:[1,0] neg_lo:[1,0]
	s_nop 0
	v_pk_fma_f32 v[36:37], v[36:37], v[212:213], v[66:67] op_sel_hi:[0,1,1]
	v_add_u32_e32 v50, 0x1200, v16
	v_ashrrev_i32_e32 v51, 31, v50
	v_lshl_add_u64 v[50:51], v[50:51], 3, s[48:49]
	v_pk_add_f32 v[70:71], v[20:21], v[36:37]
	v_pk_add_f32 v[20:21], v[20:21], v[36:37] neg_lo:[0,1] neg_hi:[0,1]
	s_nop 0
	v_pk_mul_f32 v[66:67], v[40:41], v[214:215] op_sel:[1,1] op_sel_hi:[1,0] neg_lo:[1,0]
	s_nop 0
	v_pk_fma_f32 v[40:41], v[40:41], v[214:215], v[66:67] op_sel_hi:[0,1,1]
	v_add_u32_e32 v50, 0x1400, v16
	v_ashrrev_i32_e32 v51, 31, v50
	v_lshl_add_u64 v[50:51], v[50:51], 3, s[48:49]
	v_pk_add_f32 v[36:37], v[22:23], v[40:41]
	v_pk_add_f32 v[22:23], v[22:23], v[40:41] neg_lo:[0,1] neg_hi:[0,1]
	s_nop 0
	v_pk_mul_f32 v[66:67], v[42:43], v[216:217] op_sel:[1,1] op_sel_hi:[1,0] neg_lo:[1,0]
	s_nop 0
	v_pk_fma_f32 v[42:43], v[42:43], v[216:217], v[66:67] op_sel_hi:[0,1,1]
	v_add_u32_e32 v50, 0x1600, v16
	v_ashrrev_i32_e32 v51, 31, v50
	v_lshl_add_u64 v[50:51], v[50:51], 3, s[48:49]
	s_nop 0
	v_pk_mul_f32 v[66:67], v[46:47], v[218:219] op_sel:[1,1] op_sel_hi:[1,0] neg_lo:[1,0]
	s_nop 0
	v_pk_fma_f32 v[46:47], v[46:47], v[218:219], v[66:67] op_sel_hi:[0,1,1]
	v_add_u32_e32 v50, 0x1800, v16
	v_ashrrev_i32_e32 v51, 31, v50
	v_lshl_add_u64 v[50:51], v[50:51], 3, s[48:49]
	s_nop 0
	v_pk_mul_f32 v[66:67], v[44:45], v[220:221] op_sel:[1,1] op_sel_hi:[1,0] neg_lo:[1,0]
	s_nop 0
	v_pk_fma_f32 v[44:45], v[44:45], v[220:221], v[66:67] op_sel_hi:[0,1,1]
	v_add_u32_e32 v50, 0x1a00, v16
	v_ashrrev_i32_e32 v51, 31, v50
	v_lshl_add_u64 v[50:51], v[50:51], 3, s[48:49]
	s_nop 0
	v_pk_mul_f32 v[66:67], v[48:49], v[222:223] op_sel:[1,1] op_sel_hi:[1,0] neg_lo:[1,0]
	s_nop 0
	v_pk_fma_f32 v[48:49], v[48:49], v[222:223], v[66:67] op_sel_hi:[0,1,1]
	v_add_u32_e32 v50, 0x1c00, v16
	v_ashrrev_i32_e32 v51, 31, v50
	v_lshl_add_u64 v[50:51], v[50:51], 3, s[48:49]
	s_nop 0
	v_pk_mul_f32 v[66:67], v[38:39], v[224:225] op_sel:[1,1] op_sel_hi:[1,0] neg_lo:[1,0]
	s_nop 0
	v_pk_fma_f32 v[38:39], v[38:39], v[224:225], v[66:67] op_sel_hi:[0,1,1]
	v_add_u32_e32 v50, 0x1e00, v16
	v_ashrrev_i32_e32 v51, 31, v50
	v_lshl_add_u64 v[50:51], v[50:51], 3, s[48:49]
	v_mov_b32_e32 v50, v226
	v_mov_b32_e32 v51, v227
	v_lshlrev_b32_e32 v190, 3, v16
	v_add_u32_e32 v190, 0x11000, v190
	global_load_dwordx2 v[196:197], v190, s[48:49] offset:-4096
	global_load_dwordx2 v[198:199], v190, s[48:49]
	v_add_u32_e32 v190, 0x2000, v190
	global_load_dwordx2 v[200:201], v190, s[48:49] offset:-4096
	global_load_dwordx2 v[202:203], v190, s[48:49]
	v_add_u32_e32 v190, 0x2000, v190
	global_load_dwordx2 v[204:205], v190, s[48:49] offset:-4096
	global_load_dwordx2 v[206:207], v190, s[48:49]
	v_add_u32_e32 v190, 0x2000, v190
	global_load_dwordx2 v[208:209], v190, s[48:49] offset:-4096
	global_load_dwordx2 v[210:211], v190, s[48:49]
	v_add_u32_e32 v190, 0x2000, v190
	global_load_dwordx2 v[212:213], v190, s[48:49] offset:-4096
	global_load_dwordx2 v[214:215], v190, s[48:49]
	v_add_u32_e32 v190, 0x2000, v190
	global_load_dwordx2 v[216:217], v190, s[48:49] offset:-4096
	global_load_dwordx2 v[218:219], v190, s[48:49]
	v_add_u32_e32 v190, 0x2000, v190
	global_load_dwordx2 v[220:221], v190, s[48:49] offset:-4096
	global_load_dwordx2 v[222:223], v190, s[48:49]
	v_add_u32_e32 v190, 0x2000, v190
	global_load_dwordx2 v[224:225], v190, s[48:49] offset:-4096
	global_load_dwordx2 v[226:227], v190, s[48:49]
	v_mov_b32_e32 v17, v165
	s_nop 0
	v_pk_mul_f32 v[66:67], v[18:19], v[50:51] op_sel:[1,1] op_sel_hi:[1,0] neg_lo:[1,0]
	s_nop 0
	v_pk_fma_f32 v[18:19], v[18:19], v[50:51], v[66:67] op_sel_hi:[0,1,1]
	v_mov_b32_e32 v50, v166
	v_mov_b32_e32 v17, v167
	v_mov_b32_e32 v66, v168
	v_mov_b32_e32 v17, v169
	s_nop 0
	v_pk_mul_f32 v[40:41], v[22:23], v[68:69] op_sel:[1,0] op_sel_hi:[0,0] neg_lo:[1,0]
	v_mov_b32_e32 v17, v171
	v_pk_fma_f32 v[22:23], v[22:23], v[50:51], v[40:41] op_sel_hi:[1,0,1]
	v_pk_add_f32 v[40:41], v[24:25], v[42:43]
	v_pk_add_f32 v[24:25], v[24:25], v[42:43] neg_lo:[0,1] neg_hi:[0,1]
	s_nop 0
	v_pk_mul_f32 v[42:43], v[24:25], v[66:67] op_sel:[1,0] op_sel_hi:[0,0] neg_lo:[1,0]
	v_mov_b32_e32 v17, v172
	v_pk_fma_f32 v[24:25], v[24:25], v[66:67], v[42:43] op_sel_hi:[1,0,1]
	v_pk_add_f32 v[42:43], v[26:27], v[46:47]
	v_pk_add_f32 v[26:27], v[26:27], v[46:47] neg_lo:[0,1] neg_hi:[0,1]
	s_nop 0
	v_pk_mul_f32 v[46:47], v[26:27], v[68:69] op_sel_hi:[1,0]
	s_nop 0
	v_pk_fma_f32 v[26:27], v[26:27], v[50:51], v[46:47] op_sel:[1,0,0] op_sel_hi:[0,0,1] neg_lo:[1,0,0]
	v_pk_add_f32 v[46:47], v[28:29], v[44:45]
	v_pk_add_f32 v[28:29], v[28:29], v[44:45] neg_lo:[0,1] neg_hi:[0,1]
	v_mov_b32_e32 v17, v177
	v_xor_b32_e32 v44, 0x80000000, v29
	v_mov_b32_e32 v45, v28
	v_pk_add_f32 v[28:29], v[30:31], v[48:49]
	v_pk_add_f32 v[30:31], v[30:31], v[48:49] neg_lo:[0,1] neg_hi:[0,1]
	s_nop 0
	v_pk_mul_f32 v[48:49], v[30:31], v[68:69] op_sel_hi:[1,0] neg_lo:[0,1] neg_hi:[0,1]
	s_nop 0
	v_pk_fma_f32 v[30:31], v[30:31], v[50:51], v[48:49] op_sel:[1,0,0] op_sel_hi:[0,0,1] neg_lo:[1,0,0]
	v_pk_add_f32 v[48:49], v[32:33], v[38:39]
	v_pk_add_f32 v[32:33], v[32:33], v[38:39] neg_lo:[0,1] neg_hi:[0,1]
	s_nop 0
	v_pk_mul_f32 v[38:39], v[32:33], v[66:67] op_sel:[1,0] op_sel_hi:[0,0] neg_lo:[1,0]
	s_nop 0
	v_pk_fma_f32 v[32:33], v[32:33], v[66:67], v[38:39] op_sel_hi:[1,0,1] neg_lo:[0,1,0] neg_hi:[0,1,0]
	v_pk_add_f32 v[38:39], v[34:35], v[18:19]
	v_pk_add_f32 v[18:19], v[34:35], v[18:19] neg_lo:[0,1] neg_hi:[0,1]
	s_nop 0
	v_pk_mul_f32 v[34:35], v[18:19], v[68:69] op_sel:[1,0] op_sel_hi:[0,0] neg_lo:[1,0]
	v_mov_b32_e32 v68, v170
	v_pk_fma_f32 v[18:19], v[18:19], v[50:51], v[34:35] op_sel_hi:[1,0,1] neg_lo:[0,1,0] neg_hi:[0,1,0]
	v_pk_add_f32 v[50:51], v[36:37], v[28:29]
	v_pk_add_f32 v[28:29], v[36:37], v[28:29] neg_lo:[0,1] neg_hi:[0,1]
	v_pk_add_f32 v[34:35], v[70:71], v[46:47]
	v_pk_mul_f32 v[36:37], v[28:29], v[66:67] op_sel:[1,0] op_sel_hi:[0,0] neg_lo:[1,0]
	v_pk_add_f32 v[46:47], v[70:71], v[46:47] neg_lo:[0,1] neg_hi:[0,1]
	v_pk_fma_f32 v[28:29], v[28:29], v[66:67], v[36:37] op_sel_hi:[1,0,1]
	v_pk_add_f32 v[36:37], v[40:41], v[48:49]
	v_pk_add_f32 v[40:41], v[40:41], v[48:49] neg_lo:[0,1] neg_hi:[0,1]
	s_nop 0
	v_xor_b32_e32 v48, 0x80000000, v41
	v_mov_b32_e32 v49, v40
	v_pk_add_f32 v[40:41], v[42:43], v[38:39]
	v_pk_add_f32 v[38:39], v[42:43], v[38:39] neg_lo:[0,1] neg_hi:[0,1]
	s_nop 0
	v_pk_mul_f32 v[42:43], v[66:67], v[38:39] op_sel:[0,1] op_sel_hi:[0,0] neg_lo:[0,1]
	v_pk_fma_f32 v[38:39], v[38:39], v[66:67], v[42:43] op_sel_hi:[1,0,1] neg_lo:[0,1,0] neg_hi:[0,1,0]
	v_pk_add_f32 v[42:43], v[34:35], v[36:37]
	v_pk_add_f32 v[34:35], v[34:35], v[36:37] neg_lo:[0,1] neg_hi:[0,1]
	v_pk_add_f32 v[36:37], v[50:51], v[40:41]
	v_pk_add_f32 v[40:41], v[50:51], v[40:41] neg_lo:[0,1] neg_hi:[0,1]
	s_nop 0
	v_xor_b32_e32 v50, 0x80000000, v41
	v_mov_b32_e32 v51, v40
	v_pk_add_f32 v[40:41], v[42:43], v[36:37]
	v_pk_add_f32 v[36:37], v[42:43], v[36:37] neg_lo:[0,1] neg_hi:[0,1]
	v_pk_add_f32 v[42:43], v[34:35], v[50:51]
	v_pk_add_f32 v[34:35], v[34:35], v[50:51] neg_lo:[0,1] neg_hi:[0,1]
	v_pk_add_f32 v[50:51], v[46:47], v[48:49]
	v_pk_add_f32 v[46:47], v[46:47], v[48:49] neg_lo:[0,1] neg_hi:[0,1]
	v_pk_add_f32 v[48:49], v[28:29], v[38:39]
	v_pk_add_f32 v[28:29], v[28:29], v[38:39] neg_lo:[0,1] neg_hi:[0,1]
	s_nop 0
	v_xor_b32_e32 v38, 0x80000000, v29
	v_mov_b32_e32 v39, v28
	v_pk_add_f32 v[28:29], v[50:51], v[48:49]
	v_pk_add_f32 v[48:49], v[50:51], v[48:49] neg_lo:[0,1] neg_hi:[0,1]
	v_pk_add_f32 v[50:51], v[46:47], v[38:39]
	v_pk_add_f32 v[38:39], v[46:47], v[38:39] neg_lo:[0,1] neg_hi:[0,1]
	v_pk_add_f32 v[46:47], v[20:21], v[44:45]
	v_pk_add_f32 v[20:21], v[20:21], v[44:45] neg_lo:[0,1] neg_hi:[0,1]
	v_pk_add_f32 v[44:45], v[22:23], v[30:31]
	v_pk_add_f32 v[22:23], v[22:23], v[30:31] neg_lo:[0,1] neg_hi:[0,1]
	s_nop 0
	v_pk_mul_f32 v[30:31], v[66:67], v[22:23] op_sel:[0,1] op_sel_hi:[0,0] neg_lo:[0,1]
	v_pk_fma_f32 v[22:23], v[66:67], v[22:23], v[30:31] op_sel_hi:[0,1,1]
	v_pk_add_f32 v[30:31], v[24:25], v[32:33]
	v_pk_add_f32 v[24:25], v[24:25], v[32:33] neg_lo:[0,1] neg_hi:[0,1]
	s_nop 0
	v_xor_b32_e32 v32, 0x80000000, v25
	v_mov_b32_e32 v33, v24
	v_pk_add_f32 v[24:25], v[26:27], v[18:19]
	v_pk_add_f32 v[18:19], v[26:27], v[18:19] neg_lo:[0,1] neg_hi:[0,1]
	s_nop 0
	v_pk_mul_f32 v[26:27], v[66:67], v[18:19] op_sel:[0,1] op_sel_hi:[0,0] neg_lo:[0,1]
	v_pk_fma_f32 v[18:19], v[66:67], v[18:19], v[26:27] op_sel_hi:[0,1,1] neg_lo:[1,0,0] neg_hi:[1,0,0]
	v_pk_add_f32 v[26:27], v[46:47], v[30:31]
	v_pk_add_f32 v[30:31], v[46:47], v[30:31] neg_lo:[0,1] neg_hi:[0,1]
	v_pk_add_f32 v[46:47], v[44:45], v[24:25]
	v_pk_add_f32 v[24:25], v[44:45], v[24:25] neg_lo:[0,1] neg_hi:[0,1]
	v_mov_b32_e32 v66, v168
	v_xor_b32_e32 v44, 0x80000000, v25
	v_mov_b32_e32 v45, v24
	v_pk_add_f32 v[24:25], v[26:27], v[46:47]
	v_pk_add_f32 v[26:27], v[26:27], v[46:47] neg_lo:[0,1] neg_hi:[0,1]
	v_pk_add_f32 v[46:47], v[30:31], v[44:45]
	v_pk_add_f32 v[30:31], v[30:31], v[44:45] neg_lo:[0,1] neg_hi:[0,1]
	v_pk_add_f32 v[44:45], v[20:21], v[32:33]
	v_pk_add_f32 v[20:21], v[20:21], v[32:33] neg_lo:[0,1] neg_hi:[0,1]
	v_pk_add_f32 v[32:33], v[22:23], v[18:19]
	v_pk_add_f32 v[18:19], v[22:23], v[18:19] neg_lo:[0,1] neg_hi:[0,1]
	s_nop 0
	v_xor_b32_e32 v22, 0x80000000, v19
	v_mov_b32_e32 v23, v18
	v_pk_add_f32 v[18:19], v[44:45], v[32:33]
	v_pk_add_f32 v[32:33], v[44:45], v[32:33] neg_lo:[0,1] neg_hi:[0,1]
	v_pk_add_f32 v[44:45], v[20:21], v[22:23]
	v_pk_add_f32 v[20:21], v[20:21], v[22:23] neg_lo:[0,1] neg_hi:[0,1]
	ds_write_b64 v10, v[40:41]
	ds_write_b64 v13, v[24:25]
	ds_write_b64 v15, v[28:29]
	ds_write_b64 v52, v[18:19]
	ds_write_b64 v53, v[42:43]
	ds_write_b64 v54, v[46:47]
	ds_write_b64 v55, v[50:51]
	ds_write_b64 v56, v[44:45]
	ds_write_b64 v57, v[36:37]
	ds_write_b64 v58, v[26:27]
	ds_write_b64 v59, v[48:49]
	ds_write_b64 v60, v[32:33]
	ds_write_b64 v61, v[34:35]
	ds_write_b64 v62, v[30:31]
	ds_write_b64 v63, v[38:39]
	ds_write_b64 v64, v[20:21]
	v_mov_b32_e32 v10, v179
	v_mov_b32_e32 v64, v166
	v_lshlrev_b32_e32 v13, 3, v17
	v_lshlrev_b32_e32 v48, 3, v10
	v_add3_u32 v10, 0, v13, v48
	v_xor_b32_e32 v13, 1, v17
	v_xor_b32_e32 v34, 8, v17
	v_xor_b32_e32 v36, 9, v17
	v_lshlrev_b32_e32 v13, 3, v13
	v_xor_b32_e32 v15, 2, v17
	v_xor_b32_e32 v24, 3, v17
	v_xor_b32_e32 v26, 4, v17
	v_xor_b32_e32 v28, 5, v17
	v_xor_b32_e32 v30, 6, v17
	v_xor_b32_e32 v32, 7, v17
	v_lshlrev_b32_e32 v34, 3, v34
	v_lshlrev_b32_e32 v36, 3, v36
	v_xor_b32_e32 v38, 10, v17
	v_xor_b32_e32 v40, 11, v17
	v_xor_b32_e32 v42, 12, v17
	v_xor_b32_e32 v44, 13, v17
	v_xor_b32_e32 v46, 14, v17
	v_xor_b32_e32 v17, 15, v17
	v_add3_u32 v13, 0, v13, v48
	v_lshlrev_b32_e32 v15, 3, v15
	v_lshlrev_b32_e32 v24, 3, v24
	v_lshlrev_b32_e32 v26, 3, v26
	v_lshlrev_b32_e32 v28, 3, v28
	v_lshlrev_b32_e32 v30, 3, v30
	v_lshlrev_b32_e32 v32, 3, v32
	v_add3_u32 v55, 0, v34, v48
	v_add3_u32 v56, 0, v36, v48
	v_lshlrev_b32_e32 v38, 3, v38
	v_lshlrev_b32_e32 v40, 3, v40
	v_lshlrev_b32_e32 v42, 3, v42
	v_lshlrev_b32_e32 v44, 3, v44
	v_lshlrev_b32_e32 v46, 3, v46
	v_lshlrev_b32_e32 v17, 3, v17
	ds_read_b64 v[18:19], v10
	ds_read_b64 v[20:21], v13
	v_add3_u32 v15, 0, v15, v48
	v_add3_u32 v50, 0, v24, v48
	v_add3_u32 v51, 0, v26, v48
	v_add3_u32 v52, 0, v28, v48
	v_add3_u32 v53, 0, v30, v48
	v_add3_u32 v54, 0, v32, v48
	ds_read_b64 v[34:35], v55
	ds_read_b64 v[36:37], v56
	v_add3_u32 v57, 0, v38, v48
	v_add3_u32 v58, 0, v40, v48
	v_add3_u32 v59, 0, v42, v48
	v_add3_u32 v60, 0, v44, v48
	v_add3_u32 v61, 0, v46, v48
	v_add3_u32 v62, 0, v17, v48
	v_mov_b32_e32 v17, v164
	ds_read_b64 v[22:23], v15
	ds_read_b64 v[24:25], v50
	ds_read_b64 v[26:27], v51
	ds_read_b64 v[28:29], v52
	ds_read_b64 v[30:31], v53
	ds_read_b64 v[32:33], v54
	ds_read_b64 v[38:39], v57
	ds_read_b64 v[40:41], v58
	ds_read_b64 v[42:43], v59
	ds_read_b64 v[44:45], v60
	ds_read_b64 v[46:47], v61
	ds_read_b64 v[48:49], v62
	s_waitcnt lgkmcnt(13)
	v_pk_add_f32 v[70:71], v[18:19], v[34:35]
	v_mov_b32_e32 v17, v165
	v_pk_add_f32 v[18:19], v[18:19], v[34:35] neg_lo:[0,1] neg_hi:[0,1]
	v_mov_b32_e32 v17, v167
	s_waitcnt lgkmcnt(12)
	v_pk_add_f32 v[34:35], v[20:21], v[36:37]
	v_pk_add_f32 v[20:21], v[20:21], v[36:37] neg_lo:[0,1] neg_hi:[0,1]
	v_mov_b32_e32 v17, v169
	s_nop 0
	v_pk_mul_f32 v[36:37], v[20:21], v[68:69] op_sel:[1,0] op_sel_hi:[0,0] neg_lo:[1,1] neg_hi:[0,1]
	v_mov_b32_e32 v17, v171
	v_pk_fma_f32 v[20:21], v[20:21], v[64:65], v[36:37] op_sel_hi:[1,0,1]
	s_waitcnt lgkmcnt(5)
	v_pk_add_f32 v[36:37], v[22:23], v[38:39]
	v_pk_add_f32 v[22:23], v[22:23], v[38:39] neg_lo:[0,1] neg_hi:[0,1]
	s_nop 0
	v_pk_mul_f32 v[38:39], v[22:23], v[66:67] op_sel:[1,0] op_sel_hi:[0,0] neg_lo:[1,1] neg_hi:[0,1]
	v_mov_b32_e32 v17, v172
	v_pk_fma_f32 v[22:23], v[22:23], v[66:67], v[38:39] op_sel_hi:[1,0,1]
	s_waitcnt lgkmcnt(4)
	v_pk_add_f32 v[38:39], v[24:25], v[40:41]
	v_pk_add_f32 v[24:25], v[24:25], v[40:41] neg_lo:[0,1] neg_hi:[0,1]
	s_nop 0
	v_pk_mul_f32 v[40:41], v[24:25], v[68:69] op_sel_hi:[1,0]
	s_nop 0
	v_pk_fma_f32 v[24:25], v[24:25], v[64:65], v[40:41] op_sel:[1,0,0] op_sel_hi:[0,0,1] neg_lo:[1,1,0] neg_hi:[0,1,0]
	s_waitcnt lgkmcnt(3)
	v_pk_add_f32 v[40:41], v[26:27], v[42:43]
	v_pk_add_f32 v[26:27], v[26:27], v[42:43] neg_lo:[0,1] neg_hi:[0,1]
	s_nop 0
	v_xor_b32_e32 v73, 0x80000000, v26
	v_mov_b32_e32 v72, v27
	s_waitcnt lgkmcnt(2)
	v_pk_add_f32 v[26:27], v[28:29], v[44:45]
	v_pk_add_f32 v[28:29], v[28:29], v[44:45] neg_lo:[0,1] neg_hi:[0,1]
	s_nop 0
	v_pk_mul_f32 v[42:43], v[28:29], v[68:69] op_sel_hi:[1,0] neg_lo:[0,1] neg_hi:[0,1]
	s_nop 0
	v_pk_fma_f32 v[28:29], v[28:29], v[64:65], v[42:43] op_sel:[1,0,0] op_sel_hi:[0,0,1] neg_lo:[1,1,0] neg_hi:[0,1,0]
	s_waitcnt lgkmcnt(1)
	v_pk_add_f32 v[42:43], v[30:31], v[46:47]
	v_pk_add_f32 v[30:31], v[30:31], v[46:47] neg_lo:[0,1] neg_hi:[0,1]
	s_nop 0
	v_pk_mul_f32 v[44:45], v[30:31], v[66:67] op_sel:[1,0] op_sel_hi:[0,0] neg_lo:[1,1] neg_hi:[0,1]
	s_nop 0
	v_pk_fma_f32 v[30:31], v[30:31], v[66:67], v[44:45] op_sel_hi:[1,0,1] neg_lo:[0,1,0] neg_hi:[0,1,0]
	s_waitcnt lgkmcnt(0)
	v_pk_add_f32 v[44:45], v[32:33], v[48:49]
	v_pk_add_f32 v[32:33], v[32:33], v[48:49] neg_lo:[0,1] neg_hi:[0,1]
	v_pk_add_f32 v[48:49], v[34:35], v[26:27]
	v_pk_add_f32 v[26:27], v[34:35], v[26:27] neg_lo:[0,1] neg_hi:[0,1]
	s_nop 0
	v_pk_mul_f32 v[34:35], v[26:27], v[66:67] op_sel:[1,0] op_sel_hi:[0,0] neg_lo:[1,1] neg_hi:[0,1]
	v_pk_fma_f32 v[26:27], v[26:27], v[66:67], v[34:35] op_sel_hi:[1,0,1]
	v_pk_add_f32 v[34:35], v[36:37], v[42:43]
	v_pk_add_f32 v[36:37], v[36:37], v[42:43] neg_lo:[0,1] neg_hi:[0,1]
	v_pk_mul_f32 v[46:47], v[32:33], v[68:69] op_sel:[1,0] op_sel_hi:[0,0] neg_lo:[1,1] neg_hi:[0,1]
	v_xor_b32_e32 v43, 0x80000000, v36
	v_mov_b32_e32 v42, v37
	v_pk_add_f32 v[36:37], v[38:39], v[44:45]
	v_pk_add_f32 v[38:39], v[38:39], v[44:45] neg_lo:[0,1] neg_hi:[0,1]
	v_pk_fma_f32 v[46:47], v[32:33], v[64:65], v[46:47] op_sel_hi:[1,0,1] neg_lo:[0,1,0] neg_hi:[0,1,0]
	v_pk_add_f32 v[32:33], v[70:71], v[40:41]
	v_pk_mul_f32 v[44:45], v[38:39], v[66:67] op_sel:[1,0] op_sel_hi:[0,0] neg_lo:[1,1] neg_hi:[0,1]
	v_pk_add_f32 v[40:41], v[70:71], v[40:41] neg_lo:[0,1] neg_hi:[0,1]
	v_pk_fma_f32 v[38:39], v[38:39], v[66:67], v[44:45] op_sel_hi:[1,0,1] neg_lo:[0,1,0] neg_hi:[0,1,0]
	v_pk_add_f32 v[44:45], v[32:33], v[34:35]
	v_pk_add_f32 v[32:33], v[32:33], v[34:35] neg_lo:[0,1] neg_hi:[0,1]
	v_pk_add_f32 v[34:35], v[48:49], v[36:37]
	v_pk_add_f32 v[36:37], v[48:49], v[36:37] neg_lo:[0,1] neg_hi:[0,1]
	v_pk_add_f32 v[64:65], v[44:45], v[34:35]
	v_xor_b32_e32 v49, 0x80000000, v36
	v_mov_b32_e32 v48, v37
	v_pk_add_f32 v[36:37], v[44:45], v[34:35] neg_lo:[0,1] neg_hi:[0,1]
	v_pk_add_f32 v[68:69], v[32:33], v[48:49]
	v_pk_add_f32 v[44:45], v[32:33], v[48:49] neg_lo:[0,1] neg_hi:[0,1]
	v_pk_add_f32 v[32:33], v[40:41], v[42:43]
	v_pk_add_f32 v[34:35], v[40:41], v[42:43] neg_lo:[0,1] neg_hi:[0,1]
	v_pk_add_f32 v[40:41], v[26:27], v[38:39]
	v_pk_add_f32 v[26:27], v[26:27], v[38:39] neg_lo:[0,1] neg_hi:[0,1]
	v_pk_add_f32 v[42:43], v[32:33], v[40:41] neg_lo:[0,1] neg_hi:[0,1]
	v_xor_b32_e32 v39, 0x80000000, v26
	v_mov_b32_e32 v38, v27
	v_pk_add_f32 v[26:27], v[32:33], v[40:41]
	v_pk_add_f32 v[40:41], v[20:21], v[28:29]
	v_pk_add_f32 v[20:21], v[20:21], v[28:29] neg_lo:[0,1] neg_hi:[0,1]
	v_pk_add_f32 v[32:33], v[34:35], v[38:39]
	v_pk_mul_f32 v[28:29], v[66:67], v[20:21] op_sel:[0,1] op_sel_hi:[0,0] neg_lo:[1,1] neg_hi:[1,0]
	v_pk_fma_f32 v[20:21], v[66:67], v[20:21], v[28:29] op_sel_hi:[0,1,1]
	v_pk_add_f32 v[28:29], v[22:23], v[30:31]
	v_pk_add_f32 v[22:23], v[22:23], v[30:31] neg_lo:[0,1] neg_hi:[0,1]
	v_pk_add_f32 v[38:39], v[34:35], v[38:39] neg_lo:[0,1] neg_hi:[0,1]
	v_xor_b32_e32 v31, 0x80000000, v22
	v_mov_b32_e32 v30, v23
	v_pk_add_f32 v[22:23], v[24:25], v[46:47]
	v_pk_add_f32 v[24:25], v[24:25], v[46:47] neg_lo:[0,1] neg_hi:[0,1]
	v_pk_add_f32 v[34:35], v[18:19], v[72:73]
	v_pk_mul_f32 v[46:47], v[66:67], v[24:25] op_sel:[0,1] op_sel_hi:[0,0] neg_lo:[1,1] neg_hi:[1,0]
	v_pk_fma_f32 v[24:25], v[66:67], v[24:25], v[46:47] op_sel_hi:[0,1,1] neg_lo:[1,0,0] neg_hi:[1,0,0]
	v_pk_add_f32 v[46:47], v[34:35], v[28:29]
	v_pk_add_f32 v[28:29], v[34:35], v[28:29] neg_lo:[0,1] neg_hi:[0,1]
	v_pk_add_f32 v[34:35], v[40:41], v[22:23]
	v_pk_add_f32 v[22:23], v[40:41], v[22:23] neg_lo:[0,1] neg_hi:[0,1]
	v_pk_add_f32 v[18:19], v[18:19], v[72:73] neg_lo:[0,1] neg_hi:[0,1]
	v_pk_add_f32 v[66:67], v[28:29], v[22:23] op_sel:[0,1] op_sel_hi:[1,0] neg_hi:[0,1]
	v_pk_add_f32 v[48:49], v[28:29], v[22:23] op_sel:[0,1] op_sel_hi:[1,0] neg_lo:[0,1]
	v_pk_add_f32 v[28:29], v[18:19], v[30:31]
	v_pk_add_f32 v[18:19], v[18:19], v[30:31] neg_lo:[0,1] neg_hi:[0,1]
	v_pk_add_f32 v[30:31], v[20:21], v[24:25]
	v_pk_add_f32 v[20:21], v[20:21], v[24:25] neg_lo:[0,1] neg_hi:[0,1]
	v_pk_add_f32 v[22:23], v[46:47], v[34:35]
	v_xor_b32_e32 v25, 0x80000000, v20
	v_add_u32_e32 v20, 0x2000, v16
	v_mov_b32_e32 v24, v21
	v_ashrrev_i32_e32 v21, 31, v20
	v_lshl_add_u64 v[20:21], v[20:21], 3, s[48:49]
	s_waitcnt vmcnt(0)
	v_pk_add_f32 v[40:41], v[46:47], v[34:35] neg_lo:[0,1] neg_hi:[0,1]
	v_pk_add_f32 v[34:35], v[18:19], v[24:25]
	v_pk_add_f32 v[18:19], v[18:19], v[24:25] neg_lo:[0,1] neg_hi:[0,1]
	v_pk_add_f32 v[70:71], v[28:29], v[30:31]
	v_pk_add_f32 v[46:47], v[28:29], v[30:31] neg_lo:[0,1] neg_hi:[0,1]
	s_nop 0
	v_pk_mul_f32 v[24:25], v[64:65], v[196:197] op_sel:[1,1] op_sel_hi:[1,0] neg_lo:[1,0]
	s_nop 0
	v_pk_fma_f32 v[20:21], v[64:65], v[196:197], v[24:25] op_sel_hi:[0,1,1]
	v_add_u32_e32 v24, 0x2200, v16
	v_ashrrev_i32_e32 v25, 31, v24
	v_lshl_add_u64 v[24:25], v[24:25], 3, s[48:49]
	s_nop 0
	v_pk_mul_f32 v[28:29], v[198:199], v[22:23] op_sel:[1,1] op_sel_hi:[0,1] neg_lo:[0,1]
	v_pk_fma_f32 v[22:23], v[198:199], v[22:23], v[28:29] op_sel_hi:[1,0,1]
	v_add_u32_e32 v24, 0x2400, v16
	v_ashrrev_i32_e32 v25, 31, v24
	v_lshl_add_u64 v[24:25], v[24:25], 3, s[48:49]
	s_nop 0
	v_pk_mul_f32 v[28:29], v[26:27], v[200:201] op_sel:[1,1] op_sel_hi:[1,0] neg_lo:[1,0]
	s_nop 0
	v_pk_fma_f32 v[24:25], v[26:27], v[200:201], v[28:29] op_sel_hi:[0,1,1]
	v_add_u32_e32 v26, 0x2600, v16
	v_ashrrev_i32_e32 v27, 31, v26
	v_lshl_add_u64 v[26:27], v[26:27], 3, s[48:49]
	s_nop 0
	v_pk_mul_f32 v[28:29], v[202:203], v[70:71] op_sel:[1,1] op_sel_hi:[0,1] neg_lo:[0,1]
	v_pk_fma_f32 v[26:27], v[202:203], v[70:71], v[28:29] op_sel_hi:[1,0,1]
	v_add_u32_e32 v28, 0x2800, v16
	v_ashrrev_i32_e32 v29, 31, v28
	v_lshl_add_u64 v[28:29], v[28:29], 3, s[48:49]
	s_nop 0
	v_pk_mul_f32 v[30:31], v[68:69], v[204:205] op_sel:[1,1] op_sel_hi:[1,0] neg_lo:[1,0]
	s_nop 0
	v_pk_fma_f32 v[28:29], v[68:69], v[204:205], v[30:31] op_sel_hi:[0,1,1]
	v_add_u32_e32 v30, 0x2a00, v16
	v_ashrrev_i32_e32 v31, 31, v30
	v_lshl_add_u64 v[30:31], v[30:31], 3, s[48:49]
	s_nop 0
	v_pk_mul_f32 v[64:65], v[206:207], v[66:67] op_sel:[1,1] op_sel_hi:[0,1] neg_lo:[0,1]
	v_pk_fma_f32 v[30:31], v[206:207], v[66:67], v[64:65] op_sel_hi:[1,0,1]
	v_add_u32_e32 v64, 0x2c00, v16
	v_ashrrev_i32_e32 v65, 31, v64
	v_lshl_add_u64 v[64:65], v[64:65], 3, s[48:49]
	s_nop 0
	v_pk_mul_f32 v[66:67], v[32:33], v[208:209] op_sel:[1,1] op_sel_hi:[1,0] neg_lo:[1,0]
	s_nop 0
	v_pk_fma_f32 v[32:33], v[32:33], v[208:209], v[66:67] op_sel_hi:[0,1,1]
	v_add_u32_e32 v64, 0x2e00, v16
	v_ashrrev_i32_e32 v65, 31, v64
	v_lshl_add_u64 v[64:65], v[64:65], 3, s[48:49]
	s_nop 0
	v_pk_mul_f32 v[66:67], v[210:211], v[34:35] op_sel:[1,1] op_sel_hi:[0,1] neg_lo:[0,1]
	v_pk_fma_f32 v[34:35], v[210:211], v[34:35], v[66:67] op_sel_hi:[1,0,1]
	v_add_u32_e32 v64, 0x3000, v16
	v_ashrrev_i32_e32 v65, 31, v64
	v_lshl_add_u64 v[64:65], v[64:65], 3, s[48:49]
	s_nop 0
	v_pk_mul_f32 v[66:67], v[36:37], v[212:213] op_sel:[1,1] op_sel_hi:[1,0] neg_lo:[1,0]
	s_nop 0
	v_pk_fma_f32 v[36:37], v[36:37], v[212:213], v[66:67] op_sel_hi:[0,1,1]
	v_add_u32_e32 v64, 0x3200, v16
	v_ashrrev_i32_e32 v65, 31, v64
	v_lshl_add_u64 v[64:65], v[64:65], 3, s[48:49]
	v_pk_add_f32 v[68:69], v[20:21], v[36:37]
	v_pk_add_f32 v[20:21], v[20:21], v[36:37] neg_lo:[0,1] neg_hi:[0,1]
	s_nop 0
	v_pk_mul_f32 v[66:67], v[40:41], v[214:215] op_sel:[1,1] op_sel_hi:[1,0] neg_lo:[1,0]
	s_nop 0
	v_pk_fma_f32 v[40:41], v[40:41], v[214:215], v[66:67] op_sel_hi:[0,1,1]
	v_add_u32_e32 v64, 0x3400, v16
	v_ashrrev_i32_e32 v65, 31, v64
	v_lshl_add_u64 v[64:65], v[64:65], 3, s[48:49]
	v_pk_add_f32 v[36:37], v[22:23], v[40:41]
	v_pk_add_f32 v[22:23], v[22:23], v[40:41] neg_lo:[0,1] neg_hi:[0,1]
	s_nop 0
	v_pk_mul_f32 v[66:67], v[42:43], v[216:217] op_sel:[1,1] op_sel_hi:[1,0] neg_lo:[1,0]
	s_nop 0
	v_pk_fma_f32 v[42:43], v[42:43], v[216:217], v[66:67] op_sel_hi:[0,1,1]
	v_add_u32_e32 v64, 0x3600, v16
	v_ashrrev_i32_e32 v65, 31, v64
	v_lshl_add_u64 v[64:65], v[64:65], 3, s[48:49]
	s_nop 0
	v_pk_mul_f32 v[66:67], v[46:47], v[218:219] op_sel:[1,1] op_sel_hi:[1,0] neg_lo:[1,0]
	s_nop 0
	v_pk_fma_f32 v[46:47], v[46:47], v[218:219], v[66:67] op_sel_hi:[0,1,1]
	v_add_u32_e32 v64, 0x3800, v16
	v_ashrrev_i32_e32 v65, 31, v64
	v_lshl_add_u64 v[64:65], v[64:65], 3, s[48:49]
	s_nop 0
	v_pk_mul_f32 v[66:67], v[44:45], v[220:221] op_sel:[1,1] op_sel_hi:[1,0] neg_lo:[1,0]
	s_nop 0
	v_pk_fma_f32 v[44:45], v[44:45], v[220:221], v[66:67] op_sel_hi:[0,1,1]
	v_add_u32_e32 v64, 0x3a00, v16
	v_ashrrev_i32_e32 v65, 31, v64
	v_lshl_add_u64 v[64:65], v[64:65], 3, s[48:49]
	s_nop 0
	v_pk_mul_f32 v[66:67], v[48:49], v[222:223] op_sel:[1,1] op_sel_hi:[1,0] neg_lo:[1,0]
	s_nop 0
	v_pk_fma_f32 v[48:49], v[48:49], v[222:223], v[66:67] op_sel_hi:[0,1,1]
	v_add_u32_e32 v64, 0x3c00, v16
	v_ashrrev_i32_e32 v65, 31, v64
	v_lshl_add_u64 v[64:65], v[64:65], 3, s[48:49]
	v_add_u32_e32 v16, 0x3e00, v16
	v_ashrrev_i32_e32 v17, 31, v16
	v_lshl_add_u64 v[16:17], v[16:17], 3, s[48:49]
	s_nop 0
	v_pk_mul_f32 v[66:67], v[38:39], v[224:225] op_sel:[1,1] op_sel_hi:[1,0] neg_lo:[1,0]
	s_nop 0
	v_pk_fma_f32 v[38:39], v[38:39], v[224:225], v[66:67] op_sel_hi:[0,1,1]
	s_nop 0
	v_pk_mul_f32 v[64:65], v[18:19], v[226:227] op_sel:[1,1] op_sel_hi:[1,0] neg_lo:[1,0]
	v_mov_b32_e32 v66, v170
	v_pk_fma_f32 v[16:17], v[18:19], v[226:227], v[64:65] op_sel_hi:[0,1,1]
	v_mov_b32_e32 v18, v164
	v_mov_b32_e32 v19, v167
	v_mov_b32_e32 v18, v165
	v_mov_b32_e32 v64, v168
	v_mov_b32_e32 v18, v166
	s_nop 0
	v_mov_b32_e32 v19, v169
	s_nop 0
	v_mov_b32_e32 v19, v171
	v_pk_mul_f32 v[40:41], v[22:23], v[66:67] op_sel:[1,0] op_sel_hi:[0,0] neg_lo:[1,0]
	v_mov_b32_e32 v19, v172
	s_nop 0
	v_pk_fma_f32 v[22:23], v[22:23], v[18:19], v[40:41] op_sel_hi:[1,0,1]
	v_pk_add_f32 v[40:41], v[24:25], v[42:43]
	v_pk_add_f32 v[24:25], v[24:25], v[42:43] neg_lo:[0,1] neg_hi:[0,1]
	s_nop 0
	v_pk_mul_f32 v[42:43], v[24:25], v[64:65] op_sel:[1,0] op_sel_hi:[0,0] neg_lo:[1,0]
	s_nop 0
	v_pk_fma_f32 v[24:25], v[24:25], v[64:65], v[42:43] op_sel_hi:[1,0,1]
	v_pk_add_f32 v[42:43], v[26:27], v[46:47]
	v_pk_add_f32 v[26:27], v[26:27], v[46:47] neg_lo:[0,1] neg_hi:[0,1]
	s_nop 0
	v_pk_mul_f32 v[46:47], v[26:27], v[66:67] op_sel_hi:[1,0]
	s_nop 0
	v_pk_fma_f32 v[26:27], v[26:27], v[18:19], v[46:47] op_sel:[1,0,0] op_sel_hi:[0,0,1] neg_lo:[1,0,0]
	v_pk_add_f32 v[46:47], v[28:29], v[44:45]
	v_pk_add_f32 v[28:29], v[28:29], v[44:45] neg_lo:[0,1] neg_hi:[0,1]
	s_nop 0
	v_xor_b32_e32 v44, 0x80000000, v29
	v_mov_b32_e32 v45, v28
	v_pk_add_f32 v[28:29], v[30:31], v[48:49]
	v_pk_add_f32 v[30:31], v[30:31], v[48:49] neg_lo:[0,1] neg_hi:[0,1]
	s_nop 0
	v_pk_mul_f32 v[48:49], v[30:31], v[66:67] op_sel_hi:[1,0] neg_lo:[0,1] neg_hi:[0,1]
	s_nop 0
	v_pk_fma_f32 v[30:31], v[30:31], v[18:19], v[48:49] op_sel:[1,0,0] op_sel_hi:[0,0,1] neg_lo:[1,0,0]
	v_pk_add_f32 v[48:49], v[32:33], v[38:39]
	v_pk_add_f32 v[32:33], v[32:33], v[38:39] neg_lo:[0,1] neg_hi:[0,1]
	s_nop 0
	v_pk_mul_f32 v[38:39], v[32:33], v[64:65] op_sel:[1,0] op_sel_hi:[0,0] neg_lo:[1,0]
	s_nop 0
	v_pk_fma_f32 v[32:33], v[32:33], v[64:65], v[38:39] op_sel_hi:[1,0,1] neg_lo:[0,1,0] neg_hi:[0,1,0]
	v_pk_add_f32 v[38:39], v[34:35], v[16:17]
	v_pk_add_f32 v[16:17], v[34:35], v[16:17] neg_lo:[0,1] neg_hi:[0,1]
	s_nop 0
	v_pk_mul_f32 v[34:35], v[16:17], v[66:67] op_sel:[1,0] op_sel_hi:[0,0] neg_lo:[1,0]
	s_nop 0
	v_pk_fma_f32 v[16:17], v[16:17], v[18:19], v[34:35] op_sel_hi:[1,0,1] neg_lo:[0,1,0] neg_hi:[0,1,0]
	v_pk_add_f32 v[18:19], v[68:69], v[46:47]
	v_pk_add_f32 v[34:35], v[68:69], v[46:47] neg_lo:[0,1] neg_hi:[0,1]
	v_pk_add_f32 v[46:47], v[36:37], v[28:29]
	v_pk_add_f32 v[28:29], v[36:37], v[28:29] neg_lo:[0,1] neg_hi:[0,1]
	s_nop 0
	v_pk_mul_f32 v[36:37], v[28:29], v[64:65] op_sel:[1,0] op_sel_hi:[0,0] neg_lo:[1,0]
	s_nop 0
	v_pk_fma_f32 v[28:29], v[28:29], v[64:65], v[36:37] op_sel_hi:[1,0,1]
	v_pk_add_f32 v[36:37], v[40:41], v[48:49]
	v_pk_add_f32 v[40:41], v[40:41], v[48:49] neg_lo:[0,1] neg_hi:[0,1]
	s_nop 0
	v_xor_b32_e32 v48, 0x80000000, v41
	v_mov_b32_e32 v49, v40
	v_pk_add_f32 v[40:41], v[42:43], v[38:39]
	v_pk_add_f32 v[38:39], v[42:43], v[38:39] neg_lo:[0,1] neg_hi:[0,1]
	s_nop 0
	v_pk_mul_f32 v[42:43], v[64:65], v[38:39] op_sel:[0,1] op_sel_hi:[0,0] neg_lo:[0,1]
	v_pk_fma_f32 v[38:39], v[38:39], v[64:65], v[42:43] op_sel_hi:[1,0,1] neg_lo:[0,1,0] neg_hi:[0,1,0]
	v_pk_add_f32 v[42:43], v[18:19], v[36:37]
	v_pk_add_f32 v[18:19], v[18:19], v[36:37] neg_lo:[0,1] neg_hi:[0,1]
	v_pk_add_f32 v[36:37], v[46:47], v[40:41]
	v_pk_add_f32 v[40:41], v[46:47], v[40:41] neg_lo:[0,1] neg_hi:[0,1]
	s_nop 0
	v_xor_b32_e32 v46, 0x80000000, v41
	v_mov_b32_e32 v47, v40
	v_pk_add_f32 v[40:41], v[42:43], v[36:37]
	v_pk_add_f32 v[36:37], v[42:43], v[36:37] neg_lo:[0,1] neg_hi:[0,1]
	v_pk_add_f32 v[42:43], v[18:19], v[46:47]
	v_pk_add_f32 v[18:19], v[18:19], v[46:47] neg_lo:[0,1] neg_hi:[0,1]
	v_pk_add_f32 v[46:47], v[34:35], v[48:49]
	v_pk_add_f32 v[34:35], v[34:35], v[48:49] neg_lo:[0,1] neg_hi:[0,1]
	v_pk_add_f32 v[48:49], v[28:29], v[38:39]
	v_pk_add_f32 v[28:29], v[28:29], v[38:39] neg_lo:[0,1] neg_hi:[0,1]
	s_nop 0
	v_xor_b32_e32 v38, 0x80000000, v29
	v_mov_b32_e32 v39, v28
	v_pk_add_f32 v[28:29], v[46:47], v[48:49]
	v_pk_add_f32 v[46:47], v[46:47], v[48:49] neg_lo:[0,1] neg_hi:[0,1]
	v_pk_add_f32 v[48:49], v[34:35], v[38:39]
	v_pk_add_f32 v[34:35], v[34:35], v[38:39] neg_lo:[0,1] neg_hi:[0,1]
	v_pk_add_f32 v[38:39], v[20:21], v[44:45]
	v_pk_add_f32 v[20:21], v[20:21], v[44:45] neg_lo:[0,1] neg_hi:[0,1]
	v_pk_add_f32 v[44:45], v[22:23], v[30:31]
	v_pk_add_f32 v[22:23], v[22:23], v[30:31] neg_lo:[0,1] neg_hi:[0,1]
	s_nop 0
	v_pk_mul_f32 v[30:31], v[64:65], v[22:23] op_sel:[0,1] op_sel_hi:[0,0] neg_lo:[0,1]
	v_pk_fma_f32 v[22:23], v[64:65], v[22:23], v[30:31] op_sel_hi:[0,1,1]
	v_pk_add_f32 v[30:31], v[24:25], v[32:33]
	v_pk_add_f32 v[24:25], v[24:25], v[32:33] neg_lo:[0,1] neg_hi:[0,1]
	s_nop 0
	v_xor_b32_e32 v32, 0x80000000, v25
	v_mov_b32_e32 v33, v24
	v_pk_add_f32 v[24:25], v[26:27], v[16:17]
	v_pk_add_f32 v[16:17], v[26:27], v[16:17] neg_lo:[0,1] neg_hi:[0,1]
	s_nop 0
	v_pk_mul_f32 v[26:27], v[64:65], v[16:17] op_sel:[0,1] op_sel_hi:[0,0] neg_lo:[0,1]
	v_pk_fma_f32 v[16:17], v[64:65], v[16:17], v[26:27] op_sel_hi:[0,1,1] neg_lo:[1,0,0] neg_hi:[1,0,0]
	v_pk_add_f32 v[26:27], v[38:39], v[30:31]
	v_pk_add_f32 v[30:31], v[38:39], v[30:31] neg_lo:[0,1] neg_hi:[0,1]
	v_pk_add_f32 v[38:39], v[44:45], v[24:25]
	v_pk_add_f32 v[24:25], v[44:45], v[24:25] neg_lo:[0,1] neg_hi:[0,1]
	s_nop 0
	v_xor_b32_e32 v44, 0x80000000, v25
	v_mov_b32_e32 v45, v24
	v_pk_add_f32 v[24:25], v[26:27], v[38:39]
	v_pk_add_f32 v[26:27], v[26:27], v[38:39] neg_lo:[0,1] neg_hi:[0,1]
	v_pk_add_f32 v[38:39], v[30:31], v[44:45]
	v_pk_add_f32 v[30:31], v[30:31], v[44:45] neg_lo:[0,1] neg_hi:[0,1]
	v_pk_add_f32 v[44:45], v[20:21], v[32:33]
	v_pk_add_f32 v[20:21], v[20:21], v[32:33] neg_lo:[0,1] neg_hi:[0,1]
	v_pk_add_f32 v[32:33], v[22:23], v[16:17]
	v_pk_add_f32 v[16:17], v[22:23], v[16:17] neg_lo:[0,1] neg_hi:[0,1]
	s_nop 0
	v_xor_b32_e32 v22, 0x80000000, v17
	v_mov_b32_e32 v23, v16
	v_pk_add_f32 v[16:17], v[44:45], v[32:33]
	v_pk_add_f32 v[32:33], v[44:45], v[32:33] neg_lo:[0,1] neg_hi:[0,1]
	v_pk_add_f32 v[44:45], v[20:21], v[22:23]
	v_pk_add_f32 v[20:21], v[20:21], v[22:23] neg_lo:[0,1] neg_hi:[0,1]
	ds_write_b64 v10, v[40:41]
	ds_write_b64 v13, v[24:25]
	ds_write_b64 v15, v[28:29]
	ds_write_b64 v50, v[16:17]
	ds_write_b64 v51, v[42:43]
	ds_write_b64 v52, v[38:39]
	ds_write_b64 v53, v[48:49]
	ds_write_b64 v54, v[44:45]
	ds_write_b64 v55, v[36:37]
	ds_write_b64 v56, v[26:27]
	ds_write_b64 v57, v[46:47]
	ds_write_b64 v58, v[32:33]
	ds_write_b64 v59, v[18:19]
	ds_write_b64 v60, v[30:31]
	ds_write_b64 v61, v[34:35]
	ds_write_b64 v62, v[20:21]
	v_mov_b32_e32 v10, v176
	v_mov_b32_e32 v50, v173
	s_waitcnt lgkmcnt(0)
	s_barrier
	v_add_u32_e32 v13, v50, v10
	v_lshl_add_u32 v13, v13, 3, 0
	ds_read2_b64 v[16:19], v13 offset1:16
	v_xad_u32 v15, v50, 1, v10
	v_lshl_add_u32 v15, v15, 3, 0
	s_waitcnt lgkmcnt(0)
	v_pk_fma_f32 v[16:17], v[16:17], 0, v[16:17] op_sel:[1,0,0] op_sel_hi:[0,0,1] neg_hi:[1,0,0]
	v_pk_fma_f32 v[22:23], v[182:183], s[92:93], v[182:183] op_sel:[1,0,0] op_sel_hi:[0,1,1]
	v_pk_mul_f32 v[24:25], v[22:23], v[18:19] op_sel:[1,1] op_sel_hi:[1,0] neg_hi:[0,1]
	s_nop 0
	v_pk_fma_f32 v[18:19], v[18:19], v[22:23], v[24:25] op_sel_hi:[1,0,1]
	v_pk_mul_f32 v[24:25], v[182:183], v[22:23] op_sel:[1,1] op_sel_hi:[0,1] neg_lo:[0,1]
	v_pk_fma_f32 v[26:27], v[182:183], v[22:23], v[24:25] op_sel_hi:[1,0,1]
	ds_read2_b64 v[22:25], v15 offset0:32 offset1:48
	s_waitcnt lgkmcnt(0)
	v_pk_mul_f32 v[28:29], v[22:23], v[26:27] op_sel:[1,1] op_sel_hi:[0,1] neg_hi:[1,0]
	s_nop 0
	v_pk_fma_f32 v[22:23], v[22:23], v[26:27], v[28:29] op_sel_hi:[1,0,1]
	v_pk_mul_f32 v[28:29], v[182:183], v[26:27] op_sel:[1,1] op_sel_hi:[0,1] neg_lo:[0,1]
	v_pk_fma_f32 v[26:27], v[182:183], v[26:27], v[28:29] op_sel_hi:[1,0,1]
	s_nop 0
	v_pk_mul_f32 v[28:29], v[24:25], v[26:27] op_sel:[1,1] op_sel_hi:[0,1] neg_hi:[1,0]
	s_nop 0
	v_pk_fma_f32 v[24:25], v[24:25], v[26:27], v[28:29] op_sel_hi:[1,0,1]
	v_pk_mul_f32 v[28:29], v[182:183], v[26:27] op_sel:[1,1] op_sel_hi:[0,1] neg_lo:[0,1]
	v_pk_fma_f32 v[26:27], v[182:183], v[26:27], v[28:29] op_sel_hi:[1,0,1]
	v_xad_u32 v28, v50, 2, v10
	v_lshl_add_u32 v51, v28, 3, 0
	ds_read2_b64 v[28:31], v51 offset0:64 offset1:80
	v_pk_mul_f32 v[32:33], v[182:183], v[26:27] op_sel:[1,1] op_sel_hi:[0,1] neg_lo:[0,1]
	s_waitcnt lgkmcnt(0)
	v_pk_mul_f32 v[34:35], v[28:29], v[26:27] op_sel:[1,1] op_sel_hi:[0,1] neg_hi:[1,0]
	s_nop 0
	v_pk_fma_f32 v[28:29], v[28:29], v[26:27], v[34:35] op_sel_hi:[1,0,1]
	v_pk_fma_f32 v[34:35], v[182:183], v[26:27], v[32:33] op_sel_hi:[1,0,1]
	s_nop 0
	v_pk_mul_f32 v[26:27], v[30:31], v[34:35] op_sel:[1,1] op_sel_hi:[0,1] neg_hi:[1,0]
	v_pk_fma_f32 v[26:27], v[30:31], v[34:35], v[26:27] op_sel_hi:[1,0,1]
	v_xad_u32 v30, v50, 3, v10
	v_lshl_add_u32 v54, v30, 3, 0
	ds_read2_b64 v[30:33], v54 offset0:96 offset1:112
	v_pk_mul_f32 v[36:37], v[182:183], v[34:35] op_sel:[1,1] op_sel_hi:[0,1] neg_lo:[0,1]
	v_pk_fma_f32 v[34:35], v[182:183], v[34:35], v[36:37] op_sel_hi:[1,0,1]
	s_waitcnt lgkmcnt(0)
	v_pk_mul_f32 v[36:37], v[30:31], v[34:35] op_sel:[1,1] op_sel_hi:[0,1] neg_hi:[1,0]
	s_nop 0
	v_pk_fma_f32 v[30:31], v[30:31], v[34:35], v[36:37] op_sel_hi:[1,0,1]
	v_pk_mul_f32 v[36:37], v[182:183], v[34:35] op_sel:[1,1] op_sel_hi:[0,1] neg_lo:[0,1]
	v_pk_fma_f32 v[34:35], v[182:183], v[34:35], v[36:37] op_sel_hi:[1,0,1]
	s_nop 0
	v_pk_mul_f32 v[36:37], v[32:33], v[34:35] op_sel:[1,1] op_sel_hi:[0,1] neg_hi:[1,0]
	s_nop 0
	v_pk_fma_f32 v[32:33], v[32:33], v[34:35], v[36:37] op_sel_hi:[1,0,1]
	v_pk_mul_f32 v[36:37], v[182:183], v[34:35] op_sel:[1,1] op_sel_hi:[0,1] neg_lo:[0,1]
	v_pk_fma_f32 v[38:39], v[182:183], v[34:35], v[36:37] op_sel_hi:[1,0,1]
	v_xad_u32 v34, v50, 4, v10
	v_lshl_add_u32 v55, v34, 3, 0
	ds_read2_b64 v[34:37], v55 offset0:128 offset1:144
	v_pk_mul_f32 v[40:41], v[182:183], v[38:39] op_sel:[1,1] op_sel_hi:[0,1] neg_lo:[0,1]
	s_waitcnt lgkmcnt(0)
	v_pk_mul_f32 v[42:43], v[34:35], v[38:39] op_sel:[1,1] op_sel_hi:[0,1] neg_hi:[1,0]
	s_nop 0
	v_pk_fma_f32 v[34:35], v[34:35], v[38:39], v[42:43] op_sel_hi:[1,0,1]
	v_pk_fma_f32 v[42:43], v[182:183], v[38:39], v[40:41] op_sel_hi:[1,0,1]
	s_nop 0
	v_pk_mul_f32 v[38:39], v[36:37], v[42:43] op_sel:[1,1] op_sel_hi:[0,1] neg_hi:[1,0]
	v_pk_fma_f32 v[36:37], v[36:37], v[42:43], v[38:39] op_sel_hi:[1,0,1]
	v_xad_u32 v38, v50, 5, v10
	v_lshl_add_u32 v56, v38, 3, 0
	ds_read2_b64 v[38:41], v56 offset0:160 offset1:176
	v_pk_mul_f32 v[44:45], v[182:183], v[42:43] op_sel:[1,1] op_sel_hi:[0,1] neg_lo:[0,1]
	v_pk_fma_f32 v[42:43], v[182:183], v[42:43], v[44:45] op_sel_hi:[1,0,1]
	s_waitcnt lgkmcnt(0)
	v_pk_mul_f32 v[44:45], v[38:39], v[42:43] op_sel:[1,1] op_sel_hi:[0,1] neg_hi:[1,0]
	s_nop 0
	v_pk_fma_f32 v[38:39], v[38:39], v[42:43], v[44:45] op_sel_hi:[1,0,1]
	v_pk_mul_f32 v[44:45], v[182:183], v[42:43] op_sel:[1,1] op_sel_hi:[0,1] neg_lo:[0,1]
	v_pk_fma_f32 v[42:43], v[182:183], v[42:43], v[44:45] op_sel_hi:[1,0,1]
	s_nop 0
	v_pk_mul_f32 v[44:45], v[40:41], v[42:43] op_sel:[1,1] op_sel_hi:[0,1] neg_hi:[1,0]
	s_nop 0
	v_pk_fma_f32 v[40:41], v[40:41], v[42:43], v[44:45] op_sel_hi:[1,0,1]
	v_pk_mul_f32 v[44:45], v[182:183], v[42:43] op_sel:[1,1] op_sel_hi:[0,1] neg_lo:[0,1]
	v_pk_fma_f32 v[42:43], v[182:183], v[42:43], v[44:45] op_sel_hi:[1,0,1]
	v_xad_u32 v44, v50, 6, v10
	v_lshl_add_u32 v57, v44, 3, 0
	ds_read2_b64 v[44:47], v57 offset0:192 offset1:208
	v_pk_mul_f32 v[48:49], v[182:183], v[42:43] op_sel:[1,1] op_sel_hi:[0,1] neg_lo:[0,1]
	s_waitcnt lgkmcnt(0)
	v_pk_mul_f32 v[52:53], v[44:45], v[42:43] op_sel:[1,1] op_sel_hi:[0,1] neg_hi:[1,0]
	s_nop 0
	v_pk_fma_f32 v[44:45], v[44:45], v[42:43], v[52:53] op_sel_hi:[1,0,1]
	v_pk_fma_f32 v[52:53], v[182:183], v[42:43], v[48:49] op_sel_hi:[1,0,1]
	s_nop 0
	v_pk_mul_f32 v[42:43], v[46:47], v[52:53] op_sel:[1,1] op_sel_hi:[0,1] neg_hi:[1,0]
	v_pk_fma_f32 v[42:43], v[46:47], v[52:53], v[42:43] op_sel_hi:[1,0,1]
	v_xad_u32 v46, v50, 7, v10
	v_lshl_add_u32 v58, v46, 3, 0
	ds_read2_b64 v[46:49], v58 offset0:224 offset1:240
	v_pk_mul_f32 v[60:61], v[182:183], v[52:53] op_sel:[1,1] op_sel_hi:[0,1] neg_lo:[0,1]
	v_pk_fma_f32 v[52:53], v[182:183], v[52:53], v[60:61] op_sel_hi:[1,0,1]
	s_waitcnt lgkmcnt(0)
	v_pk_mul_f32 v[60:61], v[46:47], v[52:53] op_sel:[1,1] op_sel_hi:[0,1] neg_hi:[1,0]
	s_nop 0
	v_pk_fma_f32 v[46:47], v[46:47], v[52:53], v[60:61] op_sel_hi:[1,0,1]
	v_pk_mul_f32 v[60:61], v[182:183], v[52:53] op_sel:[1,1] op_sel_hi:[0,1] neg_lo:[0,1]
	v_pk_fma_f32 v[52:53], v[182:183], v[52:53], v[60:61] op_sel_hi:[1,0,1]
	s_nop 0
	v_pk_mul_f32 v[60:61], v[48:49], v[52:53] op_sel:[1,1] op_sel_hi:[0,1] neg_hi:[1,0]
	s_nop 0
	v_pk_fma_f32 v[48:49], v[48:49], v[52:53], v[60:61] op_sel_hi:[1,0,1]
	v_pk_mul_f32 v[60:61], v[182:183], v[52:53] op_sel:[1,1] op_sel_hi:[0,1] neg_lo:[0,1]
	v_pk_fma_f32 v[64:65], v[182:183], v[52:53], v[60:61] op_sel_hi:[1,0,1]
	v_xad_u32 v52, v50, 8, v10
	v_lshl_add_u32 v52, v52, 3, 0
	v_add_u32_e32 v59, 0x800, v52
	ds_read2_b64 v[60:63], v59 offset1:16
	v_pk_mul_f32 v[66:67], v[182:183], v[64:65] op_sel:[1,1] op_sel_hi:[0,1] neg_lo:[0,1]
	v_pk_fma_f32 v[66:67], v[182:183], v[64:65], v[66:67] op_sel_hi:[1,0,1]
	s_waitcnt lgkmcnt(0)
	v_pk_mul_f32 v[52:53], v[60:61], v[64:65] op_sel:[1,1] op_sel_hi:[0,1] neg_hi:[1,0]
	v_pk_fma_f32 v[52:53], v[60:61], v[64:65], v[52:53] op_sel_hi:[1,0,1]
	v_pk_mul_f32 v[60:61], v[62:63], v[66:67] op_sel:[1,1] op_sel_hi:[0,1] neg_hi:[1,0]
	v_pk_fma_f32 v[70:71], v[62:63], v[66:67], v[60:61] op_sel_hi:[1,0,1]
	v_xad_u32 v60, v50, 9, v10
	v_lshl_add_u32 v60, v60, 3, 0
	v_add_u32_e32 v60, 0x800, v60
	ds_read2_b64 v[62:65], v60 offset0:32 offset1:48
	v_pk_mul_f32 v[68:69], v[182:183], v[66:67] op_sel:[1,1] op_sel_hi:[0,1] neg_lo:[0,1]
	v_pk_fma_f32 v[66:67], v[182:183], v[66:67], v[68:69] op_sel_hi:[1,0,1]
	s_waitcnt lgkmcnt(0)
	v_pk_mul_f32 v[68:69], v[62:63], v[66:67] op_sel:[1,1] op_sel_hi:[0,1] neg_hi:[1,0]
	s_nop 0
	v_pk_fma_f32 v[72:73], v[62:63], v[66:67], v[68:69] op_sel_hi:[1,0,1]
	v_pk_mul_f32 v[62:63], v[182:183], v[66:67] op_sel:[1,1] op_sel_hi:[0,1] neg_lo:[0,1]
	v_pk_fma_f32 v[62:63], v[182:183], v[66:67], v[62:63] op_sel_hi:[1,0,1]
	s_nop 0
	v_pk_mul_f32 v[66:67], v[64:65], v[62:63] op_sel:[1,1] op_sel_hi:[0,1] neg_hi:[1,0]
	s_nop 0
	v_pk_fma_f32 v[74:75], v[64:65], v[62:63], v[66:67] op_sel_hi:[1,0,1]
	v_pk_mul_f32 v[64:65], v[182:183], v[62:63] op_sel:[1,1] op_sel_hi:[0,1] neg_lo:[0,1]
	v_pk_fma_f32 v[66:67], v[182:183], v[62:63], v[64:65] op_sel_hi:[1,0,1]
	v_xad_u32 v61, v50, 10, v10
	v_lshl_add_u32 v61, v61, 3, 0
	v_add_u32_e32 v61, 0x800, v61
	ds_read2_b64 v[62:65], v61 offset0:64 offset1:80
	v_pk_mul_f32 v[68:69], v[182:183], v[66:67] op_sel:[1,1] op_sel_hi:[0,1] neg_lo:[0,1]
	v_pk_fma_f32 v[68:69], v[182:183], v[66:67], v[68:69] op_sel_hi:[1,0,1]
	s_waitcnt lgkmcnt(0)
	v_pk_mul_f32 v[76:77], v[62:63], v[66:67] op_sel:[1,1] op_sel_hi:[0,1] neg_hi:[1,0]
	v_pk_fma_f32 v[76:77], v[62:63], v[66:67], v[76:77] op_sel_hi:[1,0,1]
	v_pk_mul_f32 v[62:63], v[64:65], v[68:69] op_sel:[1,1] op_sel_hi:[0,1] neg_hi:[1,0]
	v_pk_fma_f32 v[78:79], v[64:65], v[68:69], v[62:63] op_sel_hi:[1,0,1]
	v_xad_u32 v62, v50, 11, v10
	v_lshl_add_u32 v62, v62, 3, 0
	v_add_u32_e32 v62, 0x800, v62
	ds_read2_b64 v[64:67], v62 offset0:96 offset1:112
	v_pk_mul_f32 v[80:81], v[182:183], v[68:69] op_sel:[1,1] op_sel_hi:[0,1] neg_lo:[0,1]
	v_pk_fma_f32 v[68:69], v[182:183], v[68:69], v[80:81] op_sel_hi:[1,0,1]
	s_waitcnt lgkmcnt(0)
	v_pk_mul_f32 v[80:81], v[64:65], v[68:69] op_sel:[1,1] op_sel_hi:[0,1] neg_hi:[1,0]
	s_nop 0
	v_pk_fma_f32 v[80:81], v[64:65], v[68:69], v[80:81] op_sel_hi:[1,0,1]
	v_pk_mul_f32 v[64:65], v[182:183], v[68:69] op_sel:[1,1] op_sel_hi:[0,1] neg_lo:[0,1]
	v_pk_fma_f32 v[64:65], v[182:183], v[68:69], v[64:65] op_sel_hi:[1,0,1]
	s_nop 0
	v_pk_mul_f32 v[68:69], v[66:67], v[64:65] op_sel:[1,1] op_sel_hi:[0,1] neg_hi:[1,0]
	s_nop 0
	v_pk_fma_f32 v[82:83], v[66:67], v[64:65], v[68:69] op_sel_hi:[1,0,1]
	v_pk_mul_f32 v[66:67], v[182:183], v[64:65] op_sel:[1,1] op_sel_hi:[0,1] neg_lo:[0,1]
	v_pk_fma_f32 v[68:69], v[182:183], v[64:65], v[66:67] op_sel_hi:[1,0,1]
	v_xad_u32 v63, v50, 12, v10
	v_lshl_add_u32 v63, v63, 3, 0
	v_add_u32_e32 v63, 0x800, v63
	ds_read2_b64 v[64:67], v63 offset0:128 offset1:144
	v_pk_mul_f32 v[84:85], v[182:183], v[68:69] op_sel:[1,1] op_sel_hi:[0,1] neg_lo:[0,1]
	v_pk_fma_f32 v[84:85], v[182:183], v[68:69], v[84:85] op_sel_hi:[1,0,1]
	s_waitcnt lgkmcnt(0)
	v_pk_mul_f32 v[86:87], v[64:65], v[68:69] op_sel:[1,1] op_sel_hi:[0,1] neg_hi:[1,0]
	v_pk_fma_f32 v[86:87], v[64:65], v[68:69], v[86:87] op_sel_hi:[1,0,1]
	v_pk_mul_f32 v[64:65], v[66:67], v[84:85] op_sel:[1,1] op_sel_hi:[0,1] neg_hi:[1,0]
	v_pk_fma_f32 v[88:89], v[66:67], v[84:85], v[64:65] op_sel_hi:[1,0,1]
	v_xad_u32 v64, v50, 13, v10
	v_lshl_add_u32 v64, v64, 3, 0
	v_add_u32_e32 v64, 0x800, v64
	ds_read2_b64 v[66:69], v64 offset0:160 offset1:176
	v_pk_mul_f32 v[90:91], v[182:183], v[84:85] op_sel:[1,1] op_sel_hi:[0,1] neg_lo:[0,1]
	v_pk_fma_f32 v[84:85], v[182:183], v[84:85], v[90:91] op_sel_hi:[1,0,1]
	s_waitcnt lgkmcnt(0)
	v_pk_mul_f32 v[90:91], v[66:67], v[84:85] op_sel:[1,1] op_sel_hi:[0,1] neg_hi:[1,0]
	s_nop 0
	v_pk_fma_f32 v[90:91], v[66:67], v[84:85], v[90:91] op_sel_hi:[1,0,1]
	v_pk_mul_f32 v[66:67], v[182:183], v[84:85] op_sel:[1,1] op_sel_hi:[0,1] neg_lo:[0,1]
	v_pk_fma_f32 v[66:67], v[182:183], v[84:85], v[66:67] op_sel_hi:[1,0,1]
	s_nop 0
	v_pk_mul_f32 v[84:85], v[68:69], v[66:67] op_sel:[1,1] op_sel_hi:[0,1] neg_hi:[1,0]
	s_nop 0
	v_pk_fma_f32 v[84:85], v[68:69], v[66:67], v[84:85] op_sel_hi:[1,0,1]
	v_pk_mul_f32 v[68:69], v[182:183], v[66:67] op_sel:[1,1] op_sel_hi:[0,1] neg_lo:[0,1]
	v_pk_fma_f32 v[92:93], v[182:183], v[66:67], v[68:69] op_sel_hi:[1,0,1]
	v_xad_u32 v65, v50, 14, v10
	v_lshl_add_u32 v65, v65, 3, 0
	v_add_u32_e32 v65, 0x800, v65
	ds_read2_b64 v[66:69], v65 offset0:192 offset1:208
	v_pk_mul_f32 v[94:95], v[182:183], v[92:93] op_sel:[1,1] op_sel_hi:[0,1] neg_lo:[0,1]
	v_xad_u32 v10, v50, 15, v10
	s_waitcnt lgkmcnt(0)
	v_pk_mul_f32 v[96:97], v[66:67], v[92:93] op_sel:[1,1] op_sel_hi:[0,1] neg_hi:[1,0]
	v_lshl_add_u32 v10, v10, 3, 0
	v_pk_fma_f32 v[96:97], v[66:67], v[92:93], v[96:97] op_sel_hi:[1,0,1]
	v_pk_fma_f32 v[92:93], v[182:183], v[92:93], v[94:95] op_sel_hi:[1,0,1]
	s_nop 0
	v_pk_mul_f32 v[66:67], v[68:69], v[92:93] op_sel:[1,1] op_sel_hi:[0,1] neg_hi:[1,0]
	v_add_u32_e32 v101, 0x800, v10
	v_pk_fma_f32 v[94:95], v[68:69], v[92:93], v[66:67] op_sel_hi:[1,0,1]
	ds_read2_b64 v[66:69], v101 offset0:224 offset1:240
	v_pk_mul_f32 v[98:99], v[182:183], v[92:93] op_sel:[1,1] op_sel_hi:[0,1] neg_lo:[0,1]
	v_pk_fma_f32 v[92:93], v[182:183], v[92:93], v[98:99] op_sel_hi:[1,0,1]
	s_waitcnt lgkmcnt(0)
	v_pk_mul_f32 v[98:99], v[66:67], v[92:93] op_sel:[1,1] op_sel_hi:[0,1] neg_hi:[1,0]
	s_nop 0
	v_pk_fma_f32 v[66:67], v[66:67], v[92:93], v[98:99] op_sel_hi:[1,0,1]
	v_pk_mul_f32 v[98:99], v[182:183], v[92:93] op_sel:[1,1] op_sel_hi:[0,1] neg_lo:[0,1]
	v_pk_fma_f32 v[20:21], v[182:183], v[92:93], v[98:99] op_sel_hi:[1,0,1]
	s_nop 0
	v_pk_mul_f32 v[92:93], v[68:69], v[20:21] op_sel:[1,1] op_sel_hi:[0,1] neg_hi:[1,0]
	s_nop 0
	v_pk_fma_f32 v[68:69], v[68:69], v[20:21], v[92:93] op_sel_hi:[1,0,1]
	v_mov_b32_e32 v10, v164
	v_pk_add_f32 v[104:105], v[16:17], v[52:53]
	v_pk_add_f32 v[16:17], v[16:17], v[52:53] neg_lo:[0,1] neg_hi:[0,1]
	v_pk_add_f32 v[52:53], v[18:19], v[70:71]
	v_pk_add_f32 v[18:19], v[18:19], v[70:71] neg_lo:[0,1] neg_hi:[0,1]
	v_mov_b32_e32 v92, v165
	v_mov_b32_e32 v20, v166
	v_mov_b32_e32 v98, v167
	v_mov_b32_e32 v10, v168
	v_mov_b32_e32 v100, v169
	v_mov_b32_e32 v50, v170
	v_mov_b32_e32 v102, v171
	v_mov_b32_e32 v21, v172
	v_pk_mul_f32 v[70:71], v[102:103], v[18:19] op_sel:[0,1] op_sel_hi:[0,0] neg_lo:[0,1]
	v_pk_fma_f32 v[18:19], v[92:93], v[18:19], v[70:71] op_sel_hi:[0,1,1]
	v_pk_add_f32 v[70:71], v[22:23], v[72:73]
	v_pk_add_f32 v[22:23], v[22:23], v[72:73] neg_lo:[0,1] neg_hi:[0,1]
	s_nop 0
	v_pk_mul_f32 v[72:73], v[50:51], v[22:23] op_sel:[0,1] op_sel_hi:[0,0] neg_lo:[0,1]
	v_pk_fma_f32 v[22:23], v[20:21], v[22:23], v[72:73] op_sel_hi:[0,1,1]
	v_pk_add_f32 v[72:73], v[24:25], v[74:75]
	v_pk_add_f32 v[24:25], v[24:25], v[74:75] neg_lo:[0,1] neg_hi:[0,1]
	s_nop 0
	v_pk_mul_f32 v[74:75], v[100:101], v[24:25] op_sel:[0,1] op_sel_hi:[0,0] neg_lo:[0,1]
	v_pk_fma_f32 v[24:25], v[98:99], v[24:25], v[74:75] op_sel_hi:[0,1,1]
	v_pk_add_f32 v[74:75], v[28:29], v[76:77]
	v_pk_add_f32 v[28:29], v[28:29], v[76:77] neg_lo:[0,1] neg_hi:[0,1]
	s_nop 0
	v_pk_mul_f32 v[76:77], v[10:11], v[28:29] op_sel:[0,1] op_sel_hi:[0,0] neg_lo:[0,1]
	v_pk_fma_f32 v[28:29], v[10:11], v[28:29], v[76:77] op_sel_hi:[0,1,1]
	v_pk_add_f32 v[76:77], v[26:27], v[78:79]
	v_pk_add_f32 v[26:27], v[26:27], v[78:79] neg_lo:[0,1] neg_hi:[0,1]
	s_nop 0
	v_pk_mul_f32 v[78:79], v[98:99], v[26:27] op_sel:[0,1] op_sel_hi:[0,0] neg_lo:[0,1]
	v_pk_fma_f32 v[26:27], v[100:101], v[26:27], v[78:79] op_sel_hi:[0,1,1]
	v_pk_add_f32 v[78:79], v[30:31], v[80:81]
	v_pk_add_f32 v[30:31], v[30:31], v[80:81] neg_lo:[0,1] neg_hi:[0,1]
	s_nop 0
	v_pk_mul_f32 v[80:81], v[20:21], v[30:31] op_sel:[0,1] op_sel_hi:[0,0] neg_lo:[0,1]
	v_pk_fma_f32 v[30:31], v[50:51], v[30:31], v[80:81] op_sel_hi:[0,1,1]
	v_pk_add_f32 v[80:81], v[32:33], v[82:83]
	v_pk_add_f32 v[32:33], v[32:33], v[82:83] neg_lo:[0,1] neg_hi:[0,1]
	s_nop 0
	v_pk_mul_f32 v[82:83], v[92:93], v[32:33] op_sel:[0,1] op_sel_hi:[0,0] neg_lo:[0,1]
	v_pk_fma_f32 v[32:33], v[102:103], v[32:33], v[82:83] op_sel_hi:[0,1,1]
	v_pk_add_f32 v[82:83], v[34:35], v[86:87]
	v_pk_add_f32 v[34:35], v[34:35], v[86:87] neg_lo:[0,1] neg_hi:[0,1]
	s_nop 0
	v_xor_b32_e32 v86, 0x80000000, v35
	v_mov_b32_e32 v87, v34
	v_pk_add_f32 v[34:35], v[36:37], v[88:89]
	v_pk_add_f32 v[36:37], v[36:37], v[88:89] neg_lo:[0,1] neg_hi:[0,1]
	s_nop 0
	v_pk_mul_f32 v[88:89], v[92:93], v[36:37] op_sel:[0,1] op_sel_hi:[0,0] neg_lo:[0,1]
	v_pk_fma_f32 v[36:37], v[102:103], v[36:37], v[88:89] op_sel_hi:[0,1,1] neg_lo:[1,0,0] neg_hi:[1,0,0]
	v_pk_add_f32 v[88:89], v[38:39], v[90:91]
	v_pk_add_f32 v[38:39], v[38:39], v[90:91] neg_lo:[0,1] neg_hi:[0,1]
	s_nop 0
	v_pk_mul_f32 v[90:91], v[20:21], v[38:39] op_sel:[0,1] op_sel_hi:[0,0] neg_lo:[0,1]
	v_pk_fma_f32 v[38:39], v[50:51], v[38:39], v[90:91] op_sel_hi:[0,1,1] neg_lo:[1,0,0] neg_hi:[1,0,0]
	v_pk_add_f32 v[90:91], v[40:41], v[84:85]
	v_pk_add_f32 v[40:41], v[40:41], v[84:85] neg_lo:[0,1] neg_hi:[0,1]
	s_nop 0
	v_pk_mul_f32 v[84:85], v[98:99], v[40:41] op_sel:[0,1] op_sel_hi:[0,0] neg_lo:[0,1]
	v_pk_fma_f32 v[40:41], v[100:101], v[40:41], v[84:85] op_sel_hi:[0,1,1] neg_lo:[1,0,0] neg_hi:[1,0,0]
	v_pk_add_f32 v[84:85], v[44:45], v[96:97]
	v_pk_add_f32 v[44:45], v[44:45], v[96:97] neg_lo:[0,1] neg_hi:[0,1]
	s_nop 0
	v_pk_mul_f32 v[96:97], v[10:11], v[44:45] op_sel:[0,1] op_sel_hi:[0,0] neg_lo:[0,1]
	v_pk_fma_f32 v[44:45], v[10:11], v[44:45], v[96:97] op_sel_hi:[0,1,1] neg_lo:[1,0,0] neg_hi:[1,0,0]
	v_pk_add_f32 v[96:97], v[42:43], v[94:95]
	v_pk_add_f32 v[42:43], v[42:43], v[94:95] neg_lo:[0,1] neg_hi:[0,1]
	s_nop 0
	v_pk_mul_f32 v[94:95], v[100:101], v[42:43] op_sel:[0,1] op_sel_hi:[0,0] neg_lo:[0,1]
	v_pk_fma_f32 v[42:43], v[98:99], v[42:43], v[94:95] op_sel_hi:[0,1,1] neg_lo:[1,0,0] neg_hi:[1,0,0]
	v_pk_add_f32 v[94:95], v[46:47], v[66:67]
	v_pk_add_f32 v[46:47], v[46:47], v[66:67] neg_lo:[0,1] neg_hi:[0,1]
	s_nop 0
	v_pk_mul_f32 v[66:67], v[50:51], v[46:47] op_sel:[0,1] op_sel_hi:[0,0] neg_lo:[0,1]
	v_pk_fma_f32 v[46:47], v[20:21], v[46:47], v[66:67] op_sel_hi:[0,1,1] neg_lo:[1,0,0] neg_hi:[1,0,0]
	v_pk_add_f32 v[66:67], v[48:49], v[68:69]
	v_pk_add_f32 v[48:49], v[48:49], v[68:69] neg_lo:[0,1] neg_hi:[0,1]
	s_nop 0
	v_pk_mul_f32 v[68:69], v[102:103], v[48:49] op_sel:[0,1] op_sel_hi:[0,0] neg_lo:[0,1]
	v_pk_fma_f32 v[48:49], v[92:93], v[48:49], v[68:69] op_sel_hi:[0,1,1] neg_lo:[1,0,0] neg_hi:[1,0,0]
	v_pk_add_f32 v[92:93], v[52:53], v[34:35]
	v_pk_add_f32 v[34:35], v[52:53], v[34:35] neg_lo:[0,1] neg_hi:[0,1]
	v_pk_add_f32 v[68:69], v[104:105], v[82:83]
	v_pk_mul_f32 v[52:53], v[50:51], v[34:35] op_sel:[0,1] op_sel_hi:[0,0] neg_lo:[0,1]
	v_pk_fma_f32 v[34:35], v[20:21], v[34:35], v[52:53] op_sel_hi:[0,1,1]
	v_pk_add_f32 v[52:53], v[70:71], v[88:89]
	v_pk_add_f32 v[70:71], v[70:71], v[88:89] neg_lo:[0,1] neg_hi:[0,1]
	v_pk_add_f32 v[82:83], v[104:105], v[82:83] neg_lo:[0,1] neg_hi:[0,1]
	v_pk_mul_f32 v[88:89], v[10:11], v[70:71] op_sel:[0,1] op_sel_hi:[0,0] neg_lo:[0,1]
	v_pk_fma_f32 v[70:71], v[10:11], v[70:71], v[88:89] op_sel_hi:[0,1,1]
	v_pk_add_f32 v[88:89], v[72:73], v[90:91]
	v_pk_add_f32 v[72:73], v[72:73], v[90:91] neg_lo:[0,1] neg_hi:[0,1]
	s_nop 0
	v_pk_mul_f32 v[90:91], v[20:21], v[72:73] op_sel:[0,1] op_sel_hi:[0,0] neg_lo:[0,1]
	v_pk_fma_f32 v[72:73], v[50:51], v[72:73], v[90:91] op_sel_hi:[0,1,1]
	v_pk_add_f32 v[90:91], v[74:75], v[84:85]
	v_pk_add_f32 v[74:75], v[74:75], v[84:85] neg_lo:[0,1] neg_hi:[0,1]
	s_nop 0
	v_xor_b32_e32 v84, 0x80000000, v75
	v_mov_b32_e32 v85, v74
	v_pk_add_f32 v[74:75], v[76:77], v[96:97]
	v_pk_add_f32 v[76:77], v[76:77], v[96:97] neg_lo:[0,1] neg_hi:[0,1]
	s_nop 0
	v_pk_mul_f32 v[96:97], v[20:21], v[76:77] op_sel:[0,1] op_sel_hi:[0,0] neg_lo:[0,1]
	v_pk_fma_f32 v[76:77], v[50:51], v[76:77], v[96:97] op_sel_hi:[0,1,1] neg_lo:[1,0,0] neg_hi:[1,0,0]
	v_pk_add_f32 v[96:97], v[78:79], v[94:95]
	v_pk_add_f32 v[78:79], v[78:79], v[94:95] neg_lo:[0,1] neg_hi:[0,1]
	s_nop 0
	v_pk_mul_f32 v[94:95], v[10:11], v[78:79] op_sel:[0,1] op_sel_hi:[0,0] neg_lo:[0,1]
	v_pk_fma_f32 v[78:79], v[10:11], v[78:79], v[94:95] op_sel_hi:[0,1,1] neg_lo:[1,0,0] neg_hi:[1,0,0]
	v_pk_add_f32 v[94:95], v[80:81], v[66:67]
	v_pk_add_f32 v[66:67], v[80:81], v[66:67] neg_lo:[0,1] neg_hi:[0,1]
	s_nop 0
	v_pk_mul_f32 v[80:81], v[50:51], v[66:67] op_sel:[0,1] op_sel_hi:[0,0] neg_lo:[0,1]
	v_pk_fma_f32 v[66:67], v[20:21], v[66:67], v[80:81] op_sel_hi:[0,1,1] neg_lo:[1,0,0] neg_hi:[1,0,0]
	v_pk_add_f32 v[80:81], v[68:69], v[90:91]
	v_pk_add_f32 v[68:69], v[68:69], v[90:91] neg_lo:[0,1] neg_hi:[0,1]
	v_pk_add_f32 v[90:91], v[92:93], v[74:75]
	v_pk_add_f32 v[74:75], v[92:93], v[74:75] neg_lo:[0,1] neg_hi:[0,1]
	s_nop 0
	v_pk_mul_f32 v[92:93], v[10:11], v[74:75] op_sel:[0,1] op_sel_hi:[0,0] neg_lo:[0,1]
	v_pk_fma_f32 v[74:75], v[10:11], v[74:75], v[92:93] op_sel_hi:[0,1,1]
	v_pk_add_f32 v[92:93], v[52:53], v[96:97]
	v_pk_add_f32 v[52:53], v[52:53], v[96:97] neg_lo:[0,1] neg_hi:[0,1]
	s_nop 0
	v_xor_b32_e32 v96, 0x80000000, v53
	v_mov_b32_e32 v97, v52
	v_pk_add_f32 v[52:53], v[88:89], v[94:95]
	v_pk_add_f32 v[88:89], v[88:89], v[94:95] neg_lo:[0,1] neg_hi:[0,1]
	s_nop 0
	v_pk_mul_f32 v[94:95], v[10:11], v[88:89] op_sel:[0,1] op_sel_hi:[0,0] neg_lo:[0,1]
	v_pk_fma_f32 v[88:89], v[10:11], v[88:89], v[94:95] op_sel_hi:[0,1,1] neg_lo:[1,0,0] neg_hi:[1,0,0]
	v_pk_add_f32 v[94:95], v[80:81], v[92:93]
	v_pk_add_f32 v[80:81], v[80:81], v[92:93] neg_lo:[0,1] neg_hi:[0,1]
	v_pk_add_f32 v[92:93], v[90:91], v[52:53]
	v_pk_add_f32 v[52:53], v[90:91], v[52:53] neg_lo:[0,1] neg_hi:[0,1]
	s_nop 0
	v_xor_b32_e32 v90, 0x80000000, v53
	v_mov_b32_e32 v91, v52
	v_pk_add_f32 v[52:53], v[94:95], v[92:93]
	v_pk_add_f32 v[92:93], v[94:95], v[92:93] neg_lo:[0,1] neg_hi:[0,1]
	v_pk_add_f32 v[94:95], v[80:81], v[90:91]
	v_pk_add_f32 v[80:81], v[80:81], v[90:91] neg_lo:[0,1] neg_hi:[0,1]
	v_pk_add_f32 v[90:91], v[68:69], v[96:97]
	v_pk_add_f32 v[68:69], v[68:69], v[96:97] neg_lo:[0,1] neg_hi:[0,1]
	v_pk_add_f32 v[96:97], v[74:75], v[88:89]
	v_pk_add_f32 v[74:75], v[74:75], v[88:89] neg_lo:[0,1] neg_hi:[0,1]
	s_nop 0
	v_xor_b32_e32 v88, 0x80000000, v75
	v_mov_b32_e32 v89, v74
	v_pk_add_f32 v[74:75], v[90:91], v[96:97]
	v_pk_add_f32 v[90:91], v[90:91], v[96:97] neg_lo:[0,1] neg_hi:[0,1]
	v_pk_add_f32 v[96:97], v[68:69], v[88:89]
	v_pk_add_f32 v[68:69], v[68:69], v[88:89] neg_lo:[0,1] neg_hi:[0,1]
	v_pk_add_f32 v[88:89], v[82:83], v[84:85]
	v_pk_add_f32 v[82:83], v[82:83], v[84:85] neg_lo:[0,1] neg_hi:[0,1]
	v_pk_add_f32 v[84:85], v[34:35], v[76:77]
	v_pk_add_f32 v[34:35], v[34:35], v[76:77] neg_lo:[0,1] neg_hi:[0,1]
	s_nop 0
	v_pk_mul_f32 v[76:77], v[10:11], v[34:35] op_sel:[0,1] op_sel_hi:[0,0] neg_lo:[0,1]
	v_pk_fma_f32 v[34:35], v[10:11], v[34:35], v[76:77] op_sel_hi:[0,1,1]
	v_pk_add_f32 v[76:77], v[70:71], v[78:79]
	v_pk_add_f32 v[70:71], v[70:71], v[78:79] neg_lo:[0,1] neg_hi:[0,1]
	s_nop 0
	v_xor_b32_e32 v78, 0x80000000, v71
	v_mov_b32_e32 v79, v70
	v_pk_add_f32 v[70:71], v[72:73], v[66:67]
	v_pk_add_f32 v[66:67], v[72:73], v[66:67] neg_lo:[0,1] neg_hi:[0,1]
	s_nop 0
	v_pk_mul_f32 v[72:73], v[10:11], v[66:67] op_sel:[0,1] op_sel_hi:[0,0] neg_lo:[0,1]
	v_pk_fma_f32 v[66:67], v[10:11], v[66:67], v[72:73] op_sel_hi:[0,1,1] neg_lo:[1,0,0] neg_hi:[1,0,0]
	v_pk_add_f32 v[72:73], v[88:89], v[76:77]
	v_pk_add_f32 v[76:77], v[88:89], v[76:77] neg_lo:[0,1] neg_hi:[0,1]
	v_pk_add_f32 v[88:89], v[84:85], v[70:71]
	v_pk_add_f32 v[70:71], v[84:85], v[70:71] neg_lo:[0,1] neg_hi:[0,1]
	s_nop 0
	v_xor_b32_e32 v84, 0x80000000, v71
	v_mov_b32_e32 v85, v70
	v_pk_add_f32 v[70:71], v[72:73], v[88:89]
	v_pk_add_f32 v[72:73], v[72:73], v[88:89] neg_lo:[0,1] neg_hi:[0,1]
	v_pk_add_f32 v[88:89], v[76:77], v[84:85]
	v_pk_add_f32 v[76:77], v[76:77], v[84:85] neg_lo:[0,1] neg_hi:[0,1]
	v_pk_add_f32 v[84:85], v[82:83], v[78:79]
	v_pk_add_f32 v[78:79], v[82:83], v[78:79] neg_lo:[0,1] neg_hi:[0,1]
	v_pk_add_f32 v[82:83], v[34:35], v[66:67]
	v_pk_add_f32 v[34:35], v[34:35], v[66:67] neg_lo:[0,1] neg_hi:[0,1]
	s_nop 0
	v_xor_b32_e32 v66, 0x80000000, v35
	v_mov_b32_e32 v67, v34
	v_pk_add_f32 v[34:35], v[84:85], v[82:83]
	v_pk_add_f32 v[82:83], v[84:85], v[82:83] neg_lo:[0,1] neg_hi:[0,1]
	v_pk_add_f32 v[84:85], v[78:79], v[66:67]
	v_pk_add_f32 v[66:67], v[78:79], v[66:67] neg_lo:[0,1] neg_hi:[0,1]
	v_pk_add_f32 v[78:79], v[16:17], v[86:87]
	v_pk_add_f32 v[16:17], v[16:17], v[86:87] neg_lo:[0,1] neg_hi:[0,1]
	v_pk_add_f32 v[86:87], v[18:19], v[36:37]
	v_pk_add_f32 v[18:19], v[18:19], v[36:37] neg_lo:[0,1] neg_hi:[0,1]
	s_nop 0
	v_pk_mul_f32 v[36:37], v[50:51], v[18:19] op_sel:[0,1] op_sel_hi:[0,0] neg_lo:[0,1]
	v_pk_fma_f32 v[18:19], v[20:21], v[18:19], v[36:37] op_sel_hi:[0,1,1]
	v_pk_add_f32 v[36:37], v[22:23], v[38:39]
	v_pk_add_f32 v[22:23], v[22:23], v[38:39] neg_lo:[0,1] neg_hi:[0,1]
	s_nop 0
	v_pk_mul_f32 v[38:39], v[10:11], v[22:23] op_sel:[0,1] op_sel_hi:[0,0] neg_lo:[0,1]
	v_pk_fma_f32 v[22:23], v[10:11], v[22:23], v[38:39] op_sel_hi:[0,1,1]
	v_pk_add_f32 v[38:39], v[24:25], v[40:41]
	v_pk_add_f32 v[24:25], v[24:25], v[40:41] neg_lo:[0,1] neg_hi:[0,1]
	s_nop 0
	v_pk_mul_f32 v[40:41], v[20:21], v[24:25] op_sel:[0,1] op_sel_hi:[0,0] neg_lo:[0,1]
	v_pk_fma_f32 v[24:25], v[50:51], v[24:25], v[40:41] op_sel_hi:[0,1,1]
	v_pk_add_f32 v[40:41], v[28:29], v[44:45]
	v_pk_add_f32 v[28:29], v[28:29], v[44:45] neg_lo:[0,1] neg_hi:[0,1]
	s_nop 0
	v_xor_b32_e32 v44, 0x80000000, v29
	v_mov_b32_e32 v45, v28
	v_pk_add_f32 v[28:29], v[26:27], v[42:43]
	v_pk_add_f32 v[26:27], v[26:27], v[42:43] neg_lo:[0,1] neg_hi:[0,1]
	s_nop 0
	v_pk_mul_f32 v[42:43], v[20:21], v[26:27] op_sel:[0,1] op_sel_hi:[0,0] neg_lo:[0,1]
	v_pk_fma_f32 v[26:27], v[50:51], v[26:27], v[42:43] op_sel_hi:[0,1,1] neg_lo:[1,0,0] neg_hi:[1,0,0]
	v_pk_add_f32 v[42:43], v[30:31], v[46:47]
	v_pk_add_f32 v[30:31], v[30:31], v[46:47] neg_lo:[0,1] neg_hi:[0,1]
	s_nop 0
	v_pk_mul_f32 v[46:47], v[10:11], v[30:31] op_sel:[0,1] op_sel_hi:[0,0] neg_lo:[0,1]
	v_pk_fma_f32 v[30:31], v[10:11], v[30:31], v[46:47] op_sel_hi:[0,1,1] neg_lo:[1,0,0] neg_hi:[1,0,0]
	v_pk_add_f32 v[46:47], v[32:33], v[48:49]
	v_pk_add_f32 v[32:33], v[32:33], v[48:49] neg_lo:[0,1] neg_hi:[0,1]
	s_nop 0
	v_pk_mul_f32 v[48:49], v[50:51], v[32:33] op_sel:[0,1] op_sel_hi:[0,0] neg_lo:[0,1]
	v_pk_fma_f32 v[20:21], v[20:21], v[32:33], v[48:49] op_sel_hi:[0,1,1] neg_lo:[1,0,0] neg_hi:[1,0,0]
	v_pk_add_f32 v[48:49], v[86:87], v[28:29]
	v_pk_add_f32 v[28:29], v[86:87], v[28:29] neg_lo:[0,1] neg_hi:[0,1]
	v_pk_add_f32 v[32:33], v[78:79], v[40:41]
	v_pk_add_f32 v[40:41], v[78:79], v[40:41] neg_lo:[0,1] neg_hi:[0,1]
	v_pk_mul_f32 v[78:79], v[10:11], v[28:29] op_sel:[0,1] op_sel_hi:[0,0] neg_lo:[0,1]
	v_pk_fma_f32 v[28:29], v[10:11], v[28:29], v[78:79] op_sel_hi:[0,1,1]
	v_pk_add_f32 v[78:79], v[36:37], v[42:43]
	v_pk_add_f32 v[36:37], v[36:37], v[42:43] neg_lo:[0,1] neg_hi:[0,1]
	s_nop 0
	v_xor_b32_e32 v42, 0x80000000, v37
	v_mov_b32_e32 v43, v36
	v_pk_add_f32 v[36:37], v[38:39], v[46:47]
	v_pk_add_f32 v[38:39], v[38:39], v[46:47] neg_lo:[0,1] neg_hi:[0,1]
	s_nop 0
	v_pk_mul_f32 v[46:47], v[10:11], v[38:39] op_sel:[0,1] op_sel_hi:[0,0] neg_lo:[0,1]
	v_pk_fma_f32 v[38:39], v[10:11], v[38:39], v[46:47] op_sel_hi:[0,1,1] neg_lo:[1,0,0] neg_hi:[1,0,0]
	v_pk_add_f32 v[46:47], v[32:33], v[78:79]
	v_pk_add_f32 v[32:33], v[32:33], v[78:79] neg_lo:[0,1] neg_hi:[0,1]
	v_pk_add_f32 v[78:79], v[48:49], v[36:37]
	v_pk_add_f32 v[36:37], v[48:49], v[36:37] neg_lo:[0,1] neg_hi:[0,1]
	s_nop 0
	v_pk_add_f32 v[86:87], v[32:33], v[36:37] op_sel:[0,1] op_sel_hi:[1,0] neg_lo:[0,1]
	v_pk_add_f32 v[32:33], v[32:33], v[36:37] op_sel:[0,1] op_sel_hi:[1,0] neg_hi:[0,1]
	v_pk_add_f32 v[48:49], v[40:41], v[42:43]
	v_pk_add_f32 v[40:41], v[40:41], v[42:43] neg_lo:[0,1] neg_hi:[0,1]
	v_pk_add_f32 v[42:43], v[28:29], v[38:39]
	v_pk_add_f32 v[28:29], v[28:29], v[38:39] neg_lo:[0,1] neg_hi:[0,1]
	v_pk_add_f32 v[36:37], v[46:47], v[78:79] neg_lo:[0,1] neg_hi:[0,1]
	v_xor_b32_e32 v38, 0x80000000, v29
	v_mov_b32_e32 v39, v28
	v_pk_add_f32 v[28:29], v[48:49], v[42:43]
	v_pk_add_f32 v[42:43], v[48:49], v[42:43] neg_lo:[0,1] neg_hi:[0,1]
	v_pk_add_f32 v[48:49], v[40:41], v[38:39]
	v_pk_add_f32 v[38:39], v[40:41], v[38:39] neg_lo:[0,1] neg_hi:[0,1]
	v_pk_add_f32 v[40:41], v[16:17], v[44:45]
	v_pk_add_f32 v[16:17], v[16:17], v[44:45] neg_lo:[0,1] neg_hi:[0,1]
	v_pk_add_f32 v[44:45], v[18:19], v[26:27]
	v_pk_add_f32 v[18:19], v[18:19], v[26:27] neg_lo:[0,1] neg_hi:[0,1]
	s_nop 0
	v_pk_mul_f32 v[26:27], v[10:11], v[18:19] op_sel:[0,1] op_sel_hi:[0,0] neg_lo:[0,1]
	v_pk_fma_f32 v[18:19], v[10:11], v[18:19], v[26:27] op_sel_hi:[0,1,1]
	v_pk_add_f32 v[26:27], v[22:23], v[30:31]
	v_pk_add_f32 v[22:23], v[22:23], v[30:31] neg_lo:[0,1] neg_hi:[0,1]
	s_nop 0
	v_xor_b32_e32 v30, 0x80000000, v23
	v_mov_b32_e32 v31, v22
	v_pk_add_f32 v[22:23], v[24:25], v[20:21]
	v_pk_add_f32 v[20:21], v[24:25], v[20:21] neg_lo:[0,1] neg_hi:[0,1]
	s_nop 0
	v_pk_mul_f32 v[24:25], v[10:11], v[20:21] op_sel:[0,1] op_sel_hi:[0,0] neg_lo:[0,1]
	v_pk_fma_f32 v[20:21], v[10:11], v[20:21], v[24:25] op_sel_hi:[0,1,1] neg_lo:[1,0,0] neg_hi:[1,0,0]
	v_pk_add_f32 v[24:25], v[40:41], v[26:27]
	v_pk_add_f32 v[26:27], v[40:41], v[26:27] neg_lo:[0,1] neg_hi:[0,1]
	v_pk_add_f32 v[40:41], v[44:45], v[22:23]
	v_pk_add_f32 v[22:23], v[44:45], v[22:23] neg_lo:[0,1] neg_hi:[0,1]
	s_nop 0
	v_xor_b32_e32 v44, 0x80000000, v23
	v_mov_b32_e32 v45, v22
	v_pk_add_f32 v[22:23], v[24:25], v[40:41]
	v_pk_add_f32 v[24:25], v[24:25], v[40:41] neg_lo:[0,1] neg_hi:[0,1]
	v_pk_add_f32 v[40:41], v[26:27], v[44:45]
	v_pk_add_f32 v[26:27], v[26:27], v[44:45] neg_lo:[0,1] neg_hi:[0,1]
	v_pk_add_f32 v[44:45], v[16:17], v[30:31]
	v_pk_add_f32 v[16:17], v[16:17], v[30:31] neg_lo:[0,1] neg_hi:[0,1]
	v_pk_add_f32 v[30:31], v[18:19], v[20:21]
	v_pk_add_f32 v[18:19], v[18:19], v[20:21] neg_lo:[0,1] neg_hi:[0,1]
	s_nop 0
	v_xor_b32_e32 v20, 0x80000000, v19
	v_mov_b32_e32 v21, v18
	v_pk_add_f32 v[18:19], v[44:45], v[30:31]
	v_pk_add_f32 v[30:31], v[44:45], v[30:31] neg_lo:[0,1] neg_hi:[0,1]
	v_pk_add_f32 v[44:45], v[16:17], v[20:21]
	v_pk_add_f32 v[16:17], v[16:17], v[20:21] neg_lo:[0,1] neg_hi:[0,1]
	v_pk_add_f32 v[20:21], v[46:47], v[78:79]
	ds_write2_b64 v13, v[52:53], v[20:21] offset1:16
	ds_write2_b64 v15, v[70:71], v[22:23] offset0:32 offset1:48
	ds_write2_b64 v51, v[74:75], v[28:29] offset0:64 offset1:80
	ds_write2_b64 v54, v[34:35], v[18:19] offset0:96 offset1:112
	ds_write2_b64 v55, v[94:95], v[86:87] offset0:128 offset1:144
	ds_write2_b64 v56, v[88:89], v[40:41] offset0:160 offset1:176
	ds_write2_b64 v57, v[96:97], v[48:49] offset0:192 offset1:208
	ds_write2_b64 v58, v[84:85], v[44:45] offset0:224 offset1:240
	ds_write2_b64 v59, v[92:93], v[36:37] offset1:16
	ds_write2_b64 v60, v[72:73], v[24:25] offset0:32 offset1:48
	ds_write2_b64 v61, v[90:91], v[42:43] offset0:64 offset1:80
	ds_write2_b64 v62, v[82:83], v[30:31] offset0:96 offset1:112
	ds_write2_b64 v63, v[80:81], v[32:33] offset0:128 offset1:144
	ds_write2_b64 v64, v[76:77], v[26:27] offset0:160 offset1:176
	ds_write2_b64 v65, v[68:69], v[38:39] offset0:192 offset1:208
	ds_write2_b64 v101, v[66:67], v[16:17] offset0:224 offset1:240
	v_mov_b32_e32 v10, v174
	s_waitcnt lgkmcnt(0)
	s_barrier
	v_lshl_add_u32 v10, v10, 3, 0
	ds_read_b64 v[16:17], v10
	ds_read_b64 v[80:81], v10 offset:4224
	ds_read_b64 v[78:79], v10 offset:8448
	ds_read_b64 v[76:77], v10 offset:12672
	ds_read_b64 v[74:75], v10 offset:16896
	ds_read_b64 v[72:73], v10 offset:21120
	ds_read_b64 v[70:71], v10 offset:25344
	ds_read_b64 v[68:69], v10 offset:29568
	ds_read_b64 v[24:25], v10 offset:33792
	ds_read_b64 v[62:63], v10 offset:38016
	ds_read_b64 v[60:61], v10 offset:42240
	ds_read_b64 v[58:59], v10 offset:46464
	ds_read_b64 v[54:55], v10 offset:50688
	ds_read_b64 v[50:51], v10 offset:54912
	ds_read_b64 v[46:47], v10 offset:59136
	ds_read_b64 v[44:45], v10 offset:63360
	v_add_u32_e32 v13, 0x10800, v10
	v_add_u32_e32 v15, 0x11880, v10
	v_add_u32_e32 v20, 0x12900, v10
	v_add_u32_e32 v21, 0x13980, v10
	ds_read_b64 v[18:19], v13
	ds_read_b64 v[66:67], v15
	ds_read_b64 v[64:65], v20
	ds_read_b64 v[38:39], v21
	v_add_u32_e32 v13, 0x14a00, v10
	v_add_u32_e32 v15, 0x15a80, v10
	v_add_u32_e32 v20, 0x16b00, v10
	v_add_u32_e32 v21, 0x17b80, v10
	ds_read_b64 v[30:31], v13
	ds_read_b64 v[56:57], v15
	ds_read_b64 v[52:53], v20
	ds_read_b64 v[48:49], v21
	v_add_u32_e32 v13, 0x18c00, v10
	v_add_u32_e32 v15, 0x19c80, v10
	v_add_u32_e32 v20, 0x1ad00, v10
	v_add_u32_e32 v21, 0x1bd80, v10
	ds_read_b64 v[82:83], v13
	ds_read_b64 v[42:43], v15
	ds_read_b64 v[40:41], v20
	ds_read_b64 v[36:37], v21
	v_add_u32_e32 v13, 0x1ce00, v10
	v_add_u32_e32 v15, 0x1de80, v10
	v_add_u32_e32 v20, 0x1ef00, v10
	v_add_u32_e32 v10, 0x1ff80, v10
	ds_read_b64 v[34:35], v13
	ds_read_b64 v[32:33], v15
	ds_read_b64 v[28:29], v20
	ds_read_b64 v[26:27], v10
	v_pk_fma_f32 v[84:85], v[180:181], s[92:93], v[180:181] op_sel:[1,0,0] op_sel_hi:[0,1,1]
	v_pk_mul_f32 v[20:21], v[180:181], v[84:85] op_sel:[1,1] op_sel_hi:[0,1] neg_lo:[0,1]
	v_pk_fma_f32 v[86:87], v[180:181], v[84:85], v[20:21] op_sel_hi:[1,0,1]
	v_mov_b32_e32 v10, v164
	v_pk_mul_f32 v[20:21], v[180:181], v[86:87] op_sel:[1,1] op_sel_hi:[0,1] neg_lo:[0,1]
	v_pk_fma_f32 v[88:89], v[180:181], v[86:87], v[20:21] op_sel_hi:[1,0,1]
	s_waitcnt lgkmcnt(14)
	v_fmac_f32_e32 v16, 0, v17
	v_pk_mul_f32 v[20:21], v[180:181], v[88:89] op_sel:[1,1] op_sel_hi:[0,1] neg_lo:[0,1]
	v_pk_fma_f32 v[90:91], v[180:181], v[88:89], v[20:21] op_sel_hi:[1,0,1]
	v_mov_b32_e32 v10, v165
	v_pk_mul_f32 v[20:21], v[180:181], v[90:91] op_sel:[1,1] op_sel_hi:[0,1] neg_lo:[0,1]
	v_pk_fma_f32 v[92:93], v[180:181], v[90:91], v[20:21] op_sel_hi:[1,0,1]
	v_mov_b32_e32 v13, v172
	v_pk_mul_f32 v[20:21], v[180:181], v[92:93] op_sel:[1,1] op_sel_hi:[0,1] neg_lo:[0,1]
	v_pk_fma_f32 v[94:95], v[180:181], v[92:93], v[20:21] op_sel_hi:[1,0,1]
	v_readlane_b32 s72, v251, 48
	v_pk_mul_f32 v[20:21], v[180:181], v[94:95] op_sel:[1,1] op_sel_hi:[0,1] neg_lo:[0,1]
	v_pk_fma_f32 v[96:97], v[180:181], v[94:95], v[20:21] op_sel_hi:[1,0,1]
	v_readlane_b32 s73, v251, 49
	v_pk_mul_f32 v[20:21], v[180:181], v[96:97] op_sel:[1,1] op_sel_hi:[0,1] neg_lo:[0,1]
	v_pk_fma_f32 v[98:99], v[180:181], v[96:97], v[20:21] op_sel_hi:[1,0,1]
	s_movk_i32 s10, 0xda00
	v_pk_mul_f32 v[20:21], v[180:181], v[98:99] op_sel:[1,1] op_sel_hi:[0,1] neg_lo:[0,1]
	v_pk_fma_f32 v[100:101], v[180:181], v[98:99], v[20:21] op_sel_hi:[1,0,1]
	s_mov_b32 s20, 0x3f61c598
	v_pk_mul_f32 v[20:21], v[180:181], v[100:101] op_sel:[1,1] op_sel_hi:[0,1] neg_lo:[0,1]
	v_pk_fma_f32 v[102:103], v[180:181], v[100:101], v[20:21] op_sel_hi:[1,0,1]
	s_mov_b32 s52, s95
	v_pk_mul_f32 v[20:21], v[180:181], v[102:103] op_sel:[1,1] op_sel_hi:[0,1] neg_lo:[0,1]
	v_pk_fma_f32 v[104:105], v[180:181], v[102:103], v[20:21] op_sel_hi:[1,0,1]
	s_mov_b32 s53, s94
	v_pk_mul_f32 v[20:21], v[180:181], v[104:105] op_sel:[1,1] op_sel_hi:[0,1] neg_lo:[0,1]
	v_pk_fma_f32 v[106:107], v[180:181], v[104:105], v[20:21] op_sel_hi:[1,0,1]
	s_mov_b32 s21, 0xbef15aea
	v_pk_mul_f32 v[20:21], v[180:181], v[106:107] op_sel:[1,1] op_sel_hi:[0,1] neg_lo:[0,1]
	v_pk_fma_f32 v[108:109], v[180:181], v[106:107], v[20:21] op_sel_hi:[1,0,1]
	s_mov_b32 s40, s47
	v_pk_mul_f32 v[20:21], v[180:181], v[108:109] op_sel:[1,1] op_sel_hi:[0,1] neg_lo:[0,1]
	v_pk_fma_f32 v[110:111], v[180:181], v[108:109], v[20:21] op_sel_hi:[1,0,1]
	s_mov_b32 s41, s42
	v_pk_mul_f32 v[20:21], v[180:181], v[110:111] op_sel:[1,1] op_sel_hi:[0,1] neg_lo:[0,1]
	v_pk_fma_f32 v[112:113], v[180:181], v[110:111], v[20:21] op_sel_hi:[1,0,1]
	s_mov_b32 s38, 0x3f3504f3
	v_pk_mul_f32 v[20:21], v[180:181], v[112:113] op_sel:[1,1] op_sel_hi:[0,1] neg_lo:[0,1]
	v_pk_fma_f32 v[20:21], v[180:181], v[112:113], v[20:21] op_sel_hi:[1,0,1]
	s_mov_b32 s39, 0xbf3504f3
	v_pk_mul_f32 v[114:115], v[180:181], v[20:21] op_sel:[1,1] op_sel_hi:[0,1] neg_lo:[0,1]
	v_pk_fma_f32 v[114:115], v[180:181], v[20:21], v[114:115] op_sel_hi:[1,0,1]
	v_mul_f32_e32 v18, v18, v20
	v_pk_mul_f32 v[116:117], v[180:181], v[114:115] op_sel:[1,1] op_sel_hi:[0,1] neg_lo:[0,1]
	v_pk_fma_f32 v[116:117], v[180:181], v[114:115], v[116:117] op_sel_hi:[1,0,1]
	v_fmac_f32_e32 v18, v19, v21
	v_pk_mul_f32 v[118:119], v[180:181], v[116:117] op_sel:[1,1] op_sel_hi:[0,1] neg_lo:[0,1]
	v_pk_fma_f32 v[118:119], v[180:181], v[116:117], v[118:119] op_sel_hi:[1,0,1]
	v_add_f32_e32 v17, v16, v18
	v_pk_mul_f32 v[120:121], v[180:181], v[118:119] op_sel:[1,1] op_sel_hi:[0,1] neg_lo:[0,1]
	v_pk_fma_f32 v[120:121], v[180:181], v[118:119], v[120:121] op_sel_hi:[1,0,1]
	s_mov_b32 s28, 0x3f226799
	v_pk_mul_f32 v[122:123], v[180:181], v[120:121] op_sel:[1,1] op_sel_hi:[0,1] neg_lo:[0,1]
	v_pk_fma_f32 v[122:123], v[180:181], v[120:121], v[122:123] op_sel_hi:[1,0,1]
	s_mov_b32 s29, 0xbf45e403
	v_pk_mul_f32 v[124:125], v[180:181], v[122:123] op_sel:[1,1] op_sel_hi:[0,1] neg_lo:[0,1]
	v_pk_fma_f32 v[124:125], v[180:181], v[122:123], v[124:125] op_sel_hi:[1,0,1]
	s_mov_b32 s82, 0x3f0e39da
	v_pk_mul_f32 v[126:127], v[180:181], v[124:125] op_sel:[1,1] op_sel_hi:[0,1] neg_lo:[0,1]
	v_pk_fma_f32 v[126:127], v[180:181], v[124:125], v[126:127] op_sel_hi:[1,0,1]
	s_mov_b32 s83, 0xbf54db31
	v_pk_mul_f32 v[128:129], v[180:181], v[126:127] op_sel:[1,1] op_sel_hi:[0,1] neg_lo:[0,1]
	v_pk_fma_f32 v[128:129], v[180:181], v[126:127], v[128:129] op_sel_hi:[1,0,1]
	s_mov_b32 s22, 0x3ef15aea
	v_pk_mul_f32 v[130:131], v[180:181], v[128:129] op_sel:[1,1] op_sel_hi:[0,1] neg_lo:[0,1]
	v_pk_fma_f32 v[130:131], v[180:181], v[128:129], v[130:131] op_sel_hi:[1,0,1]
	s_mov_b32 s23, 0xbf61c598
	v_pk_mul_f32 v[132:133], v[180:181], v[130:131] op_sel:[1,1] op_sel_hi:[0,1] neg_lo:[0,1]
	v_pk_fma_f32 v[132:133], v[180:181], v[130:131], v[132:133] op_sel_hi:[1,0,1]
	s_mov_b32 s18, 0x3ec3ef15
	v_pk_mul_f32 v[134:135], v[180:181], v[132:133] op_sel:[1,1] op_sel_hi:[0,1] neg_lo:[0,1]
	v_pk_fma_f32 v[134:135], v[180:181], v[132:133], v[134:135] op_sel_hi:[1,0,1]
	s_mov_b32 s19, 0xbf6c835e
	v_pk_mul_f32 v[136:137], v[180:181], v[134:135] op_sel:[1,1] op_sel_hi:[0,1] neg_lo:[0,1]
	v_pk_fma_f32 v[136:137], v[180:181], v[134:135], v[136:137] op_sel_hi:[1,0,1]
	s_mov_b32 s24, 0x3f54db31
	v_pk_mul_f32 v[138:139], v[180:181], v[136:137] op_sel:[1,1] op_sel_hi:[0,1] neg_lo:[0,1]
	v_pk_fma_f32 v[138:139], v[180:181], v[136:137], v[138:139] op_sel_hi:[1,0,1]
	s_mov_b32 s25, 0xbf0e39da
	v_pk_mul_f32 v[140:141], v[180:181], v[138:139] op_sel:[1,1] op_sel_hi:[0,1] neg_lo:[0,1]
	v_pk_fma_f32 v[140:141], v[180:181], v[138:139], v[140:141] op_sel_hi:[1,0,1]
	s_mov_b32 s74, 0x3f45e403
	v_pk_mul_f32 v[142:143], v[180:181], v[140:141] op_sel:[1,1] op_sel_hi:[0,1] neg_lo:[0,1]
	v_pk_fma_f32 v[22:23], v[180:181], v[140:141], v[142:143] op_sel_hi:[1,0,1]
	s_waitcnt lgkmcnt(0)
	v_pk_mul_f32 v[142:143], v[26:27], v[22:23] op_sel:[1,1] op_sel_hi:[0,1] neg_hi:[1,0]
	s_mov_b32 s75, 0xbf226799
	v_pk_fma_f32 v[26:27], v[26:27], v[22:23], v[142:143] op_sel_hi:[1,0,1]
	v_pk_mul_f32 v[22:23], v[28:29], v[140:141] op_sel:[1,1] op_sel_hi:[0,1] neg_hi:[1,0]
	s_mov_b32 s36, s77
	v_pk_fma_f32 v[28:29], v[28:29], v[140:141], v[22:23] op_sel_hi:[1,0,1]
	v_pk_mul_f32 v[22:23], v[32:33], v[138:139] op_sel:[1,1] op_sel_hi:[0,1] neg_hi:[1,0]
	s_mov_b32 s37, s43
	v_pk_fma_f32 v[32:33], v[32:33], v[138:139], v[22:23] op_sel_hi:[1,0,1]
	v_pk_mul_f32 v[22:23], v[34:35], v[136:137] op_sel:[1,1] op_sel_hi:[0,1] neg_hi:[1,0]
	s_mov_b32 s76, s43
	v_pk_fma_f32 v[34:35], v[34:35], v[136:137], v[22:23] op_sel_hi:[1,0,1]
	v_pk_mul_f32 v[22:23], v[36:37], v[134:135] op_sel:[1,1] op_sel_hi:[0,1] neg_hi:[1,0]
	s_mov_b32 s16, 0x3f6c835e
	v_pk_fma_f32 v[36:37], v[36:37], v[134:135], v[22:23] op_sel_hi:[1,0,1]
	v_pk_mul_f32 v[22:23], v[40:41], v[132:133] op_sel:[1,1] op_sel_hi:[0,1] neg_hi:[1,0]
	s_mov_b32 s17, 0xbec3ef15
	v_pk_fma_f32 v[40:41], v[40:41], v[132:133], v[22:23] op_sel_hi:[1,0,1]
	v_pk_mul_f32 v[22:23], v[42:43], v[130:131] op_sel:[1,1] op_sel_hi:[0,1] neg_hi:[1,0]
	s_mov_b32 s16, s19
	v_pk_fma_f32 v[42:43], v[42:43], v[130:131], v[22:23] op_sel_hi:[1,0,1]
	v_pk_mul_f32 v[22:23], v[82:83], v[128:129] op_sel:[1,1] op_sel_hi:[0,1] neg_hi:[1,0]
	s_mov_b32 s27, s29
	v_pk_fma_f32 v[22:23], v[82:83], v[128:129], v[22:23] op_sel_hi:[1,0,1]
	v_pk_mul_f32 v[82:83], v[48:49], v[126:127] op_sel:[1,1] op_sel_hi:[0,1] neg_hi:[1,0]
	s_mov_b32 s26, s75
	v_pk_fma_f32 v[48:49], v[48:49], v[126:127], v[82:83] op_sel_hi:[1,0,1]
	v_pk_mul_f32 v[82:83], v[52:53], v[124:125] op_sel:[1,1] op_sel_hi:[0,1] neg_hi:[1,0]
	s_mov_b32 s46, s42
	v_pk_fma_f32 v[52:53], v[52:53], v[124:125], v[82:83] op_sel_hi:[1,0,1]
	v_pk_mul_f32 v[82:83], v[56:57], v[122:123] op_sel:[1,1] op_sel_hi:[0,1] neg_hi:[1,0]
	v_mov_b32_e32 v124, v171
	v_pk_fma_f32 v[56:57], v[56:57], v[122:123], v[82:83] op_sel_hi:[1,0,1]
	v_pk_mul_f32 v[82:83], v[30:31], v[120:121] op_sel:[1,1] op_sel_hi:[0,1] neg_hi:[1,0]
	v_mov_b32_e32 v122, v169
	v_pk_fma_f32 v[30:31], v[30:31], v[120:121], v[82:83] op_sel_hi:[1,0,1]
	v_pk_mul_f32 v[82:83], v[38:39], v[118:119] op_sel:[1,1] op_sel_hi:[0,1] neg_hi:[1,0]
	v_mov_b32_e32 v120, v167
	v_pk_fma_f32 v[38:39], v[38:39], v[118:119], v[82:83] op_sel_hi:[1,0,1]
	v_pk_mul_f32 v[82:83], v[64:65], v[116:117] op_sel:[1,1] op_sel_hi:[0,1] neg_hi:[1,0]
	v_mov_b32_e32 v118, v165
	v_pk_fma_f32 v[64:65], v[64:65], v[116:117], v[82:83] op_sel_hi:[1,0,1]
	v_pk_mul_f32 v[82:83], v[66:67], v[114:115] op_sel:[1,1] op_sel_hi:[0,1] neg_hi:[1,0]
	s_nop 0
	v_pk_fma_f32 v[66:67], v[66:67], v[114:115], v[82:83] op_sel_hi:[1,0,1]
	v_pk_mul_f32 v[82:83], v[44:45], v[112:113] op_sel:[1,1] op_sel_hi:[0,1] neg_hi:[1,0]
	s_nop 0
	v_pk_fma_f32 v[44:45], v[44:45], v[112:113], v[82:83] op_sel_hi:[1,0,1]
	v_pk_mul_f32 v[82:83], v[46:47], v[110:111] op_sel:[1,1] op_sel_hi:[0,1] neg_hi:[1,0]
	s_nop 0
	v_pk_fma_f32 v[46:47], v[46:47], v[110:111], v[82:83] op_sel_hi:[1,0,1]
	v_pk_mul_f32 v[82:83], v[50:51], v[108:109] op_sel:[1,1] op_sel_hi:[0,1] neg_hi:[1,0]
	s_nop 0
	v_pk_fma_f32 v[50:51], v[50:51], v[108:109], v[82:83] op_sel_hi:[1,0,1]
	v_pk_mul_f32 v[82:83], v[54:55], v[106:107] op_sel:[1,1] op_sel_hi:[0,1] neg_hi:[1,0]
	s_nop 0
	v_pk_fma_f32 v[54:55], v[54:55], v[106:107], v[82:83] op_sel_hi:[1,0,1]
	v_pk_mul_f32 v[82:83], v[58:59], v[104:105] op_sel:[1,1] op_sel_hi:[0,1] neg_hi:[1,0]
	s_nop 0
	v_pk_fma_f32 v[58:59], v[58:59], v[104:105], v[82:83] op_sel_hi:[1,0,1]
	v_pk_mul_f32 v[82:83], v[60:61], v[102:103] op_sel:[1,1] op_sel_hi:[0,1] neg_hi:[1,0]
	s_nop 0
	v_pk_fma_f32 v[60:61], v[60:61], v[102:103], v[82:83] op_sel_hi:[1,0,1]
	v_pk_mul_f32 v[82:83], v[62:63], v[100:101] op_sel:[1,1] op_sel_hi:[0,1] neg_hi:[1,0]
	s_nop 0
	v_pk_fma_f32 v[62:63], v[62:63], v[100:101], v[82:83] op_sel_hi:[1,0,1]
	v_pk_mul_f32 v[82:83], v[24:25], v[98:99] op_sel:[1,1] op_sel_hi:[0,1] neg_hi:[1,0]
	s_nop 0
	v_pk_fma_f32 v[24:25], v[24:25], v[98:99], v[82:83] op_sel_hi:[1,0,1]
	v_pk_mul_f32 v[82:83], v[68:69], v[96:97] op_sel:[1,1] op_sel_hi:[0,1] neg_hi:[1,0]
	v_add_f32_e32 v22, v24, v22
	v_pk_fma_f32 v[68:69], v[68:69], v[96:97], v[82:83] op_sel_hi:[1,0,1]
	v_pk_mul_f32 v[82:83], v[70:71], v[94:95] op_sel:[1,1] op_sel_hi:[0,1] neg_hi:[1,0]
	v_add_f32_e32 v20, v17, v22
	v_pk_fma_f32 v[70:71], v[70:71], v[94:95], v[82:83] op_sel_hi:[1,0,1]
	v_pk_mul_f32 v[82:83], v[72:73], v[92:93] op_sel:[1,1] op_sel_hi:[0,1] neg_hi:[1,0]
	v_mov_b32_e32 v94, v171
	v_pk_fma_f32 v[72:73], v[72:73], v[92:93], v[82:83] op_sel_hi:[1,0,1]
	v_pk_mul_f32 v[82:83], v[74:75], v[90:91] op_sel:[1,1] op_sel_hi:[0,1] neg_hi:[1,0]
	v_mov_b32_e32 v92, v170
	v_pk_fma_f32 v[74:75], v[74:75], v[90:91], v[82:83] op_sel_hi:[1,0,1]
	v_pk_mul_f32 v[82:83], v[76:77], v[88:89] op_sel:[1,1] op_sel_hi:[0,1] neg_hi:[1,0]
	v_mov_b32_e32 v90, v169
	v_pk_fma_f32 v[76:77], v[76:77], v[88:89], v[82:83] op_sel_hi:[1,0,1]
	v_pk_mul_f32 v[82:83], v[78:79], v[86:87] op_sel:[1,1] op_sel_hi:[0,1] neg_hi:[1,0]
	v_mov_b32_e32 v88, v168
	v_pk_fma_f32 v[78:79], v[78:79], v[86:87], v[82:83] op_sel_hi:[1,0,1]
	v_pk_mul_f32 v[82:83], v[84:85], v[80:81] op_sel:[1,1] op_sel_hi:[1,0] neg_hi:[0,1]
	v_mov_b32_e32 v86, v167
	v_pk_fma_f32 v[80:81], v[80:81], v[84:85], v[82:83] op_sel_hi:[1,0,1]
	v_mov_b32_e32 v84, v166
	v_pk_add_f32 v[96:97], v[80:81], v[66:67]
	v_pk_add_f32 v[66:67], v[80:81], v[66:67] neg_lo:[0,1] neg_hi:[0,1]
	s_nop 0
	v_sub_f32_e32 v82, v25, v23
	v_pk_mul_f32 v[80:81], v[94:95], v[66:67] op_sel:[0,1] op_sel_hi:[0,0] neg_lo:[0,1]
	v_pk_fma_f32 v[80:81], v[10:11], v[66:67], v[80:81] op_sel_hi:[0,1,1]
	v_pk_add_f32 v[66:67], v[78:79], v[64:65]
	v_pk_add_f32 v[64:65], v[78:79], v[64:65] neg_lo:[0,1] neg_hi:[0,1]
	s_nop 0
	v_pk_mul_f32 v[78:79], v[92:93], v[64:65] op_sel:[0,1] op_sel_hi:[0,0] neg_lo:[0,1]
	v_pk_fma_f32 v[64:65], v[84:85], v[64:65], v[78:79] op_sel_hi:[0,1,1]
	v_pk_add_f32 v[78:79], v[76:77], v[38:39]
	v_pk_add_f32 v[38:39], v[76:77], v[38:39] neg_lo:[0,1] neg_hi:[0,1]
	s_barrier
	v_pk_mul_f32 v[76:77], v[90:91], v[38:39] op_sel:[0,1] op_sel_hi:[0,0] neg_lo:[0,1]
	v_pk_fma_f32 v[76:77], v[86:87], v[38:39], v[76:77] op_sel_hi:[0,1,1]
	v_pk_add_f32 v[38:39], v[74:75], v[30:31]
	v_pk_add_f32 v[30:31], v[74:75], v[30:31] neg_lo:[0,1] neg_hi:[0,1]
	s_nop 0
	v_pk_mul_f32 v[74:75], v[88:89], v[30:31] op_sel:[0,1] op_sel_hi:[0,0] neg_lo:[0,1]
	v_pk_fma_f32 v[30:31], v[88:89], v[30:31], v[74:75] op_sel_hi:[0,1,1]
	v_pk_add_f32 v[74:75], v[72:73], v[56:57]
	v_pk_add_f32 v[56:57], v[72:73], v[56:57] neg_lo:[0,1] neg_hi:[0,1]
	v_sub_f32_e32 v22, v17, v22
	v_pk_mul_f32 v[72:73], v[86:87], v[56:57] op_sel:[0,1] op_sel_hi:[0,0] neg_lo:[0,1]
	v_pk_fma_f32 v[72:73], v[90:91], v[56:57], v[72:73] op_sel_hi:[0,1,1]
	v_pk_add_f32 v[56:57], v[70:71], v[52:53]
	v_pk_add_f32 v[52:53], v[70:71], v[52:53] neg_lo:[0,1] neg_hi:[0,1]
	v_ashrrev_i32_e32 v15, 31, v14
	v_pk_mul_f32 v[70:71], v[84:85], v[52:53] op_sel:[0,1] op_sel_hi:[0,0] neg_lo:[0,1]
	v_pk_fma_f32 v[52:53], v[92:93], v[52:53], v[70:71] op_sel_hi:[0,1,1]
	v_pk_add_f32 v[70:71], v[68:69], v[48:49]
	v_pk_add_f32 v[48:49], v[68:69], v[48:49] neg_lo:[0,1] neg_hi:[0,1]
	v_lshl_add_u64 v[14:15], v[14:15], 2, s[72:73]
	v_pk_mul_f32 v[68:69], v[10:11], v[48:49] op_sel:[0,1] op_sel_hi:[0,0] neg_lo:[0,1]
	v_pk_fma_f32 v[98:99], v[94:95], v[48:49], v[68:69] op_sel_hi:[0,1,1]
	v_pk_add_f32 v[48:49], v[62:63], v[42:43]
	v_pk_add_f32 v[42:43], v[62:63], v[42:43] neg_lo:[0,1] neg_hi:[0,1]
	v_pk_add_f32 v[68:69], v[58:59], v[36:37]
	v_pk_mul_f32 v[62:63], v[10:11], v[42:43] op_sel:[0,1] op_sel_hi:[0,0] neg_lo:[0,1]
	v_pk_fma_f32 v[62:63], v[94:95], v[42:43], v[62:63] op_sel_hi:[0,1,1] neg_lo:[1,0,0] neg_hi:[1,0,0]
	v_pk_add_f32 v[42:43], v[60:61], v[40:41]
	v_pk_add_f32 v[40:41], v[60:61], v[40:41] neg_lo:[0,1] neg_hi:[0,1]
	v_pk_add_f32 v[36:37], v[58:59], v[36:37] neg_lo:[0,1] neg_hi:[0,1]
	v_pk_mul_f32 v[60:61], v[84:85], v[40:41] op_sel:[0,1] op_sel_hi:[0,0] neg_lo:[0,1]
	v_pk_fma_f32 v[60:61], v[92:93], v[40:41], v[60:61] op_sel_hi:[0,1,1] neg_lo:[1,0,0] neg_hi:[1,0,0]
	v_pk_mul_f32 v[40:41], v[86:87], v[36:37] op_sel:[0,1] op_sel_hi:[0,0] neg_lo:[0,1]
	v_pk_fma_f32 v[100:101], v[90:91], v[36:37], v[40:41] op_sel_hi:[0,1,1] neg_lo:[1,0,0] neg_hi:[1,0,0]
	v_pk_add_f32 v[40:41], v[54:55], v[34:35]
	v_pk_add_f32 v[34:35], v[54:55], v[34:35] neg_lo:[0,1] neg_hi:[0,1]
	v_add_f32_e32 v38, v38, v40
	v_pk_mul_f32 v[36:37], v[88:89], v[34:35] op_sel:[0,1] op_sel_hi:[0,0] neg_lo:[0,1]
	v_pk_fma_f32 v[34:35], v[88:89], v[34:35], v[36:37] op_sel_hi:[0,1,1] neg_lo:[1,0,0] neg_hi:[1,0,0]
	v_pk_add_f32 v[36:37], v[50:51], v[32:33]
	v_pk_add_f32 v[32:33], v[50:51], v[32:33] neg_lo:[0,1] neg_hi:[0,1]
	v_add_f32_e32 v30, v30, v34
	v_pk_mul_f32 v[50:51], v[90:91], v[32:33] op_sel:[0,1] op_sel_hi:[0,0] neg_lo:[0,1]
	v_pk_fma_f32 v[86:87], v[86:87], v[32:33], v[50:51] op_sel_hi:[0,1,1] neg_lo:[1,0,0] neg_hi:[1,0,0]
	v_pk_add_f32 v[32:33], v[46:47], v[28:29]
	v_pk_add_f32 v[28:29], v[46:47], v[28:29] neg_lo:[0,1] neg_hi:[0,1]
	v_pk_add_f32 v[50:51], v[44:45], v[26:27]
	v_pk_mul_f32 v[46:47], v[92:93], v[28:29] op_sel:[0,1] op_sel_hi:[0,0] neg_lo:[0,1]
	v_pk_add_f32 v[26:27], v[44:45], v[26:27] neg_lo:[0,1] neg_hi:[0,1]
	v_pk_fma_f32 v[46:47], v[84:85], v[28:29], v[46:47] op_sel_hi:[0,1,1] neg_lo:[1,0,0] neg_hi:[1,0,0]
	v_pk_mul_f32 v[28:29], v[94:95], v[26:27] op_sel:[0,1] op_sel_hi:[0,0] neg_lo:[0,1]
	v_pk_fma_f32 v[90:91], v[10:11], v[26:27], v[28:29] op_sel_hi:[0,1,1] neg_lo:[1,0,0] neg_hi:[1,0,0]
	v_pk_add_f32 v[28:29], v[96:97], v[48:49] neg_lo:[0,1] neg_hi:[0,1]
	v_pk_add_f32 v[26:27], v[96:97], v[48:49]
	v_pk_mul_f32 v[44:45], v[92:93], v[28:29] op_sel:[0,1] op_sel_hi:[0,0] neg_lo:[0,1]
	v_pk_fma_f32 v[94:95], v[84:85], v[28:29], v[44:45] op_sel_hi:[0,1,1]
	v_pk_add_f32 v[28:29], v[66:67], v[42:43] neg_lo:[0,1] neg_hi:[0,1]
	v_pk_add_f32 v[44:45], v[78:79], v[68:69] neg_lo:[0,1] neg_hi:[0,1]
	v_pk_add_f32 v[48:49], v[66:67], v[42:43]
	v_pk_mul_f32 v[42:43], v[88:89], v[28:29] op_sel:[0,1] op_sel_hi:[0,0] neg_lo:[0,1]
	v_pk_mul_f32 v[54:55], v[84:85], v[44:45] op_sel:[0,1] op_sel_hi:[0,0] neg_lo:[0,1]
	v_pk_fma_f32 v[28:29], v[88:89], v[28:29], v[42:43] op_sel_hi:[0,1,1]
	v_pk_add_f32 v[42:43], v[78:79], v[68:69]
	v_pk_fma_f32 v[68:69], v[92:93], v[44:45], v[54:55] op_sel_hi:[0,1,1]
	v_pk_add_f32 v[54:55], v[74:75], v[36:37]
	v_pk_add_f32 v[36:37], v[74:75], v[36:37] neg_lo:[0,1] neg_hi:[0,1]
	v_pk_add_f32 v[58:59], v[56:57], v[32:33]
	v_pk_mul_f32 v[44:45], v[84:85], v[36:37] op_sel:[0,1] op_sel_hi:[0,0] neg_lo:[0,1]
	v_pk_add_f32 v[32:33], v[56:57], v[32:33] neg_lo:[0,1] neg_hi:[0,1]
	v_pk_fma_f32 v[74:75], v[92:93], v[36:37], v[44:45] op_sel_hi:[0,1,1] neg_lo:[1,0,0] neg_hi:[1,0,0]
	v_pk_mul_f32 v[36:37], v[88:89], v[32:33] op_sel:[0,1] op_sel_hi:[0,0] neg_lo:[0,1]
	v_pk_fma_f32 v[44:45], v[88:89], v[32:33], v[36:37] op_sel_hi:[0,1,1] neg_lo:[1,0,0] neg_hi:[1,0,0]
	v_pk_add_f32 v[36:37], v[70:71], v[50:51] neg_lo:[0,1] neg_hi:[0,1]
	v_pk_add_f32 v[32:33], v[70:71], v[50:51]
	v_pk_mul_f32 v[50:51], v[92:93], v[36:37] op_sel:[0,1] op_sel_hi:[0,0] neg_lo:[0,1]
	v_pk_add_f32 v[66:67], v[26:27], v[54:55]
	v_pk_add_f32 v[26:27], v[26:27], v[54:55] neg_lo:[0,1] neg_hi:[0,1]
	v_pk_fma_f32 v[50:51], v[84:85], v[36:37], v[50:51] op_sel_hi:[0,1,1] neg_lo:[1,0,0] neg_hi:[1,0,0]
	v_pk_mul_f32 v[36:37], v[88:89], v[26:27] op_sel:[0,1] op_sel_hi:[0,0] neg_lo:[0,1]
	v_pk_add_f32 v[70:71], v[42:43], v[32:33]
	v_pk_add_f32 v[32:33], v[42:43], v[32:33] neg_lo:[0,1] neg_hi:[0,1]
	v_pk_fma_f32 v[26:27], v[88:89], v[26:27], v[36:37] op_sel_hi:[0,1,1]
	v_pk_mul_f32 v[36:37], v[88:89], v[32:33] op_sel:[0,1] op_sel_hi:[0,0] neg_lo:[0,1]
	v_pk_fma_f32 v[36:37], v[88:89], v[32:33], v[36:37] op_sel_hi:[0,1,1] neg_lo:[1,0,0] neg_hi:[1,0,0]
	v_pk_add_f32 v[32:33], v[94:95], v[74:75] neg_lo:[0,1] neg_hi:[0,1]
	v_pk_add_f32 v[56:57], v[68:69], v[50:51]
	v_pk_mul_f32 v[42:43], v[88:89], v[32:33] op_sel:[0,1] op_sel_hi:[0,0] neg_lo:[0,1]
	v_pk_fma_f32 v[32:33], v[88:89], v[32:33], v[42:43] op_sel_hi:[0,1,1]
	v_pk_add_f32 v[42:43], v[68:69], v[50:51] neg_lo:[0,1] neg_hi:[0,1]
	v_pk_add_f32 v[54:55], v[94:95], v[74:75]
	v_pk_mul_f32 v[50:51], v[88:89], v[42:43] op_sel:[0,1] op_sel_hi:[0,0] neg_lo:[0,1]
	v_pk_fma_f32 v[42:43], v[88:89], v[42:43], v[50:51] op_sel_hi:[0,1,1] neg_lo:[1,0,0] neg_hi:[1,0,0]
	v_pk_add_f32 v[50:51], v[80:81], v[62:63] neg_lo:[0,1] neg_hi:[0,1]
	v_pk_add_f32 v[74:75], v[80:81], v[62:63]
	v_pk_mul_f32 v[62:63], v[92:93], v[50:51] op_sel:[0,1] op_sel_hi:[0,0] neg_lo:[0,1]
	v_pk_fma_f32 v[94:95], v[84:85], v[50:51], v[62:63] op_sel_hi:[0,1,1]
	v_pk_add_f32 v[50:51], v[64:65], v[60:61] neg_lo:[0,1] neg_hi:[0,1]
	v_pk_add_f32 v[68:69], v[64:65], v[60:61]
	v_pk_mul_f32 v[60:61], v[88:89], v[50:51] op_sel:[0,1] op_sel_hi:[0,0] neg_lo:[0,1]
	v_pk_fma_f32 v[50:51], v[88:89], v[50:51], v[60:61] op_sel_hi:[0,1,1]
	v_pk_add_f32 v[60:61], v[76:77], v[100:101] neg_lo:[0,1] neg_hi:[0,1]
	v_pk_add_f32 v[64:65], v[76:77], v[100:101]
	v_pk_mul_f32 v[62:63], v[84:85], v[60:61] op_sel:[0,1] op_sel_hi:[0,0] neg_lo:[0,1]
	v_pk_fma_f32 v[96:97], v[92:93], v[60:61], v[62:63] op_sel_hi:[0,1,1]
	v_pk_add_f32 v[60:61], v[72:73], v[86:87] neg_lo:[0,1] neg_hi:[0,1]
	v_pk_add_f32 v[76:77], v[52:53], v[46:47]
	v_pk_add_f32 v[46:47], v[52:53], v[46:47] neg_lo:[0,1] neg_hi:[0,1]
	v_pk_add_f32 v[62:63], v[72:73], v[86:87]
	v_pk_mul_f32 v[72:73], v[84:85], v[60:61] op_sel:[0,1] op_sel_hi:[0,0] neg_lo:[0,1]
	v_pk_mul_f32 v[52:53], v[88:89], v[46:47] op_sel:[0,1] op_sel_hi:[0,0] neg_lo:[0,1]
	v_pk_fma_f32 v[86:87], v[92:93], v[60:61], v[72:73] op_sel_hi:[0,1,1] neg_lo:[1,0,0] neg_hi:[1,0,0]
	v_pk_fma_f32 v[60:61], v[88:89], v[46:47], v[52:53] op_sel_hi:[0,1,1] neg_lo:[1,0,0] neg_hi:[1,0,0]
	v_pk_add_f32 v[46:47], v[98:99], v[90:91]
	v_pk_add_f32 v[52:53], v[98:99], v[90:91] neg_lo:[0,1] neg_hi:[0,1]
	v_pk_add_f32 v[80:81], v[64:65], v[46:47]
	v_pk_add_f32 v[46:47], v[64:65], v[46:47] neg_lo:[0,1] neg_hi:[0,1]
	s_nop 0
	v_pk_mul_f32 v[64:65], v[88:89], v[46:47] op_sel:[0,1] op_sel_hi:[0,0] neg_lo:[0,1]
	v_pk_fma_f32 v[64:65], v[88:89], v[46:47], v[64:65] op_sel_hi:[0,1,1] neg_lo:[1,0,0] neg_hi:[1,0,0]
	v_pk_add_f32 v[46:47], v[94:95], v[86:87] neg_lo:[0,1] neg_hi:[0,1]
	v_pk_mul_f32 v[72:73], v[92:93], v[52:53] op_sel:[0,1] op_sel_hi:[0,0] neg_lo:[0,1]
	v_pk_add_f32 v[78:79], v[74:75], v[62:63]
	v_pk_add_f32 v[62:63], v[74:75], v[62:63] neg_lo:[0,1] neg_hi:[0,1]
	v_pk_fma_f32 v[52:53], v[84:85], v[52:53], v[72:73] op_sel_hi:[0,1,1] neg_lo:[1,0,0] neg_hi:[1,0,0]
	v_pk_mul_f32 v[74:75], v[88:89], v[46:47] op_sel:[0,1] op_sel_hi:[0,0] neg_lo:[0,1]
	v_pk_fma_f32 v[46:47], v[88:89], v[46:47], v[74:75] op_sel_hi:[0,1,1]
	v_pk_add_f32 v[74:75], v[96:97], v[52:53]
	v_pk_add_f32 v[52:53], v[96:97], v[52:53] neg_lo:[0,1] neg_hi:[0,1]
	v_sub_f32_e32 v34, v16, v18
	v_pk_mul_f32 v[84:85], v[88:89], v[52:53] op_sel:[0,1] op_sel_hi:[0,0] neg_lo:[0,1]
	v_sub_f32_e32 v25, v33, v43
	v_sub_f32_e32 v43, v31, v35
	v_sub_f32_e32 v35, v51, v61
	v_pk_fma_f32 v[52:53], v[88:89], v[52:53], v[84:85] op_sel_hi:[0,1,1] neg_lo:[1,0,0] neg_hi:[1,0,0]
	v_sub_f32_e32 v51, v34, v82
	v_sub_f32_e32 v13, v49, v59
	v_sub_f32_e32 v10, v47, v53
	v_add_f32_e32 v49, v68, v76
	v_add_f32_e32 v53, v51, v30
	v_sub_f32_e32 v23, v27, v37
	v_sub_f32_e32 v27, v55, v57
	v_add_f32_e32 v40, v78, v80
	v_add_f32_e32 v55, v53, v49
	v_add_f32_e32 v16, v55, v40
	v_sub_f32_e32 v41, v39, v41
	v_add_f32_e32 v48, v48, v58
	v_add_f32_e32 v21, v20, v38
	global_store_dword v[14:15], v16, off offset:2048
	v_add_co_u32_e32 v16, vcc, s85, v14
	v_add_f32_e32 v47, v66, v70
	v_add_f32_e32 v24, v21, v48
	v_add_f32_e32 v28, v28, v44
	v_sub_f32_e32 v44, v22, v41
	v_addc_co_u32_e32 v17, vcc, 0, v15, vcc
	v_pk_mul_f32 v[72:73], v[88:89], v[62:63] op_sel:[0,1] op_sel_hi:[0,0] neg_lo:[0,1]
	v_add_f32_e32 v19, v24, v47
	v_add_f32_e32 v54, v54, v56
	v_add_f32_e32 v56, v44, v28
	v_add_co_u32_e32 v18, vcc, s84, v14
	v_add_f32_e32 v34, v34, v82
	v_pk_fma_f32 v[62:63], v[88:89], v[62:63], v[72:73] op_sel_hi:[0,1,1]
	v_pk_add_f32 v[72:73], v[94:95], v[86:87]
	global_store_dword v[14:15], v19, off
	v_add_f32_e32 v57, v56, v54
	v_addc_co_u32_e32 v19, vcc, 0, v15, vcc
	v_add_f32_e32 v50, v50, v60
	v_sub_f32_e32 v58, v34, v43
	global_store_dword v[18:19], v57, off offset:-4096
	v_add_f32_e32 v57, v72, v74
	v_add_f32_e32 v59, v58, v50
	v_sub_f32_e32 v20, v20, v38
	v_sub_f32_e32 v37, v29, v45
	v_sub_f32_e32 v45, v69, v77
	v_add_f32_e32 v60, v59, v57
	v_add_f32_e32 v26, v26, v36
	v_sub_f32_e32 v36, v20, v13
	v_sub_f32_e32 v30, v51, v30
	global_store_dword v[16:17], v60, off offset:2048
	v_add_f32_e32 v16, v36, v26
	v_add_f32_e32 v38, v62, v64
	v_sub_f32_e32 v51, v30, v45
	global_store_dword v[18:19], v16, off
	v_add_f32_e32 v16, v51, v38
	global_store_dword v[18:19], v16, off offset:2048
	v_add_co_u32_e32 v16, vcc, s61, v14
	v_add_f32_e32 v22, v22, v41
	s_nop 0
	v_addc_co_u32_e32 v17, vcc, 0, v15, vcc
	v_add_f32_e32 v32, v32, v42
	v_sub_f32_e32 v41, v22, v37
	v_add_co_u32_e32 v18, vcc, s45, v14
	v_add_f32_e32 v42, v41, v32
	s_nop 0
	v_addc_co_u32_e32 v19, vcc, 0, v15, vcc
	v_add_f32_e32 v34, v34, v43
	global_store_dword v[18:19], v42, off offset:-4096
	v_add_f32_e32 v42, v46, v52
	v_sub_f32_e32 v43, v34, v35
	v_sub_f32_e32 v39, v67, v71
	v_add_f32_e32 v46, v43, v42
	v_sub_f32_e32 v21, v21, v48
	v_sub_f32_e32 v33, v79, v81
	global_store_dword v[16:17], v46, off offset:2048
	v_sub_f32_e32 v16, v21, v39
	v_sub_f32_e32 v46, v53, v49
	global_store_dword v[18:19], v16, off
	v_sub_f32_e32 v16, v46, v33
	global_store_dword v[18:19], v16, off offset:2048
	v_add_co_u32_e32 v16, vcc, s86, v14
	v_sub_f32_e32 v28, v44, v28
	s_nop 0
	v_addc_co_u32_e32 v17, vcc, 0, v15, vcc
	v_add_co_u32_e32 v18, vcc, s88, v14
	v_sub_f32_e32 v44, v28, v27
	s_nop 0
	v_addc_co_u32_e32 v19, vcc, 0, v15, vcc
	v_sub_f32_e32 v31, v73, v75
	global_store_dword v[18:19], v44, off offset:-4096
	v_sub_f32_e32 v44, v58, v50
	v_sub_f32_e32 v48, v44, v31
	v_add_f32_e32 v20, v20, v13
	v_sub_f32_e32 v29, v63, v65
	global_store_dword v[16:17], v48, off offset:2048
	v_sub_f32_e32 v13, v20, v23
	v_add_f32_e32 v30, v30, v45
	v_add_co_u32_e32 v16, vcc, s90, v14
	global_store_dword v[18:19], v13, off
	v_sub_f32_e32 v13, v30, v29
	v_addc_co_u32_e32 v17, vcc, 0, v15, vcc
	global_store_dword v[18:19], v13, off offset:2048
	v_add_f32_e32 v22, v22, v37
	v_add_co_u32_e32 v18, vcc, s8, v14
	v_sub_f32_e32 v13, v22, v25
	s_nop 0
	v_addc_co_u32_e32 v19, vcc, 0, v15, vcc
	global_store_dword v[18:19], v13, off offset:-4096
	v_add_f32_e32 v13, v34, v35
	v_sub_f32_e32 v34, v13, v10
	global_store_dword v[16:17], v34, off offset:2048
	v_sub_f32_e32 v16, v24, v47
	global_store_dword v[18:19], v16, off
	v_sub_f32_e32 v16, v55, v40
	global_store_dword v[18:19], v16, off offset:2048
	v_add_co_u32_e32 v16, vcc, s9, v14
	v_sub_f32_e32 v24, v56, v54
	s_nop 0
	v_addc_co_u32_e32 v17, vcc, 0, v15, vcc
	v_add_co_u32_e32 v18, vcc, s7, v14
	v_add_f32_e32 v10, v13, v10
	s_nop 0
	v_addc_co_u32_e32 v19, vcc, 0, v15, vcc
	global_store_dword v[18:19], v24, off offset:-4096
	v_sub_f32_e32 v24, v59, v57
	global_store_dword v[16:17], v24, off offset:2048
	v_sub_f32_e32 v16, v36, v26
	global_store_dword v[18:19], v16, off
	v_sub_f32_e32 v16, v51, v38
	global_store_dword v[18:19], v16, off offset:2048
	v_add_co_u32_e32 v16, vcc, s5, v14
	v_sub_f32_e32 v24, v41, v32
	s_nop 0
	v_addc_co_u32_e32 v17, vcc, 0, v15, vcc
	v_add_co_u32_e32 v18, vcc, s6, v14
	s_nop 1
	v_addc_co_u32_e32 v19, vcc, 0, v15, vcc
	global_store_dword v[18:19], v24, off offset:-4096
	v_sub_f32_e32 v24, v43, v42
	global_store_dword v[16:17], v24, off offset:2048
	v_add_f32_e32 v16, v21, v39
	global_store_dword v[18:19], v16, off
	v_add_f32_e32 v16, v46, v33
	global_store_dword v[18:19], v16, off offset:2048
	v_add_co_u32_e32 v16, vcc, s4, v14
	v_add_f32_e32 v21, v28, v27
	s_nop 0
	v_addc_co_u32_e32 v17, vcc, 0, v15, vcc
	v_add_co_u32_e32 v18, vcc, s1, v14
	s_nop 1
	v_addc_co_u32_e32 v19, vcc, 0, v15, vcc
	global_store_dword v[18:19], v21, off offset:-4096
	v_add_f32_e32 v21, v44, v31
	global_store_dword v[16:17], v21, off offset:2048
	v_add_f32_e32 v16, v20, v23
	global_store_dword v[18:19], v16, off
	v_add_f32_e32 v16, v30, v29
	v_add_co_u32_e32 v14, vcc, s0, v14
	global_store_dword v[18:19], v16, off offset:2048
	v_add_f32_e32 v16, v22, v25
	v_addc_co_u32_e32 v15, vcc, 0, v15, vcc
	global_store_dword v[14:15], v16, off
	global_store_dword v[14:15], v10, off offset:2048
	v_mov_b32_e32 v10, v184
	v_mov_b32_e32 v14, v185
	v_mov_b32_e32 v18, v1
	s_movk_i32 s0, 0xfe00
	v_sub_u32_e32 v13, 0x4000, v18
	v_cmp_eq_u32_e32 vcc, 0, v18
	v_cmp_eq_u32_e64 s[0:1], s0, v18
	v_cmp_eq_u32_e64 s[4:5], s50, v18
	v_cndmask_b32_e64 v20, v13, 0, vcc
	v_sub_u32_e32 v13, 0x3e00, v18
	v_cndmask_b32_e64 v22, v13, 0, s[0:1]
	v_sub_u32_e32 v13, 0x3c00, v18
	v_ashrrev_i32_e32 v21, 31, v20
	v_ashrrev_i32_e32 v23, 31, v22
	v_cndmask_b32_e64 v24, v13, 0, s[4:5]
	v_lshl_add_u64 v[20:21], v[20:21], 1, s[2:3]
	v_lshl_add_u64 v[22:23], v[22:23], 1, s[2:3]
	v_ashrrev_i32_e32 v25, 31, v24
	v_sub_u32_e32 v13, 0x3a00, v18
	v_cmp_eq_u32_e64 s[6:7], s51, v18
	v_lshl_add_u64 v[24:25], v[24:25], 1, s[2:3]
	global_load_ushort v15, v[20:21], off
	s_nop 0
	global_load_ushort v22, v[22:23], off
	s_nop 0
	global_load_ushort v23, v[24:25], off
	v_cndmask_b32_e64 v20, v13, 0, s[6:7]
	v_ashrrev_i32_e32 v21, 31, v20
	v_ashrrev_i32_e32 v19, 31, v18
	v_lshl_add_u64 v[20:21], v[20:21], 1, s[2:3]
	v_lshl_add_u64 v[16:17], v[18:19], 1, s[78:79]
	global_load_ushort v20, v[20:21], off
	s_nop 0
	global_load_ushort v13, v[16:17], off offset:3072
	v_sub_u32_e32 v24, 0x3800, v18
	v_sub_u32_e32 v26, 0x3600, v18
	v_sub_u32_e32 v28, 0x3400, v18
	v_sub_u32_e32 v32, 0x3200, v18
	v_cmp_eq_u32_e64 s[8:9], s60, v18
	v_cmp_eq_u32_e64 s[10:11], s10, v18
	s_mov_b32 s78, s69
	s_mov_b32 s79, s68
	s_mov_b32 s50, s21
	s_mov_b32 s51, s20
	s_mov_b32 s60, s25
	s_waitcnt vmcnt(4)
	v_lshlrev_b32_e32 v15, 16, v15
	v_cndmask_b32_e64 v19, -v15, v15, vcc
	s_waitcnt vmcnt(3)
	v_lshlrev_b32_e32 v15, 16, v22
	v_add_co_u32_e32 v22, vcc, s85, v16
	v_cndmask_b32_e64 v31, -v15, v15, s[0:1]
	s_waitcnt vmcnt(2)
	v_lshlrev_b32_e32 v15, 16, v23
	v_addc_co_u32_e32 v23, vcc, 0, v17, vcc
	v_cndmask_b32_e64 v30, -v15, v15, s[4:5]
	s_waitcnt vmcnt(1)
	v_lshlrev_b32_e32 v15, 16, v20
	v_add_co_u32_e32 v20, vcc, s84, v16
	v_cndmask_b32_e64 v15, -v15, v15, s[6:7]
	s_nop 0
	v_addc_co_u32_e32 v21, vcc, 0, v17, vcc
	v_cmp_eq_u32_e64 s[6:7], s56, v18
	v_cmp_eq_u32_e64 s[4:5], s57, v18
	v_cmp_eq_u32_e64 s[0:1], s58, v18
	v_cndmask_b32_e64 v24, v24, 0, s[6:7]
	v_cndmask_b32_e64 v26, v26, 0, s[4:5]
	v_cndmask_b32_e64 v28, v28, 0, s[0:1]
	v_cmp_eq_u32_e32 vcc, s59, v18
	v_ashrrev_i32_e32 v25, 31, v24
	v_ashrrev_i32_e32 v27, 31, v26
	v_ashrrev_i32_e32 v29, 31, v28
	v_cndmask_b32_e64 v32, v32, 0, vcc
	v_lshl_add_u64 v[24:25], v[24:25], 1, s[2:3]
	v_lshl_add_u64 v[26:27], v[26:27], 1, s[2:3]
	v_lshl_add_u64 v[28:29], v[28:29], 1, s[2:3]
	v_ashrrev_i32_e32 v33, 31, v32
	v_lshl_add_u64 v[32:33], v[32:33], 1, s[2:3]
	global_load_ushort v34, v[24:25], off
	s_nop 0
	global_load_ushort v26, v[26:27], off
	s_nop 0
	global_load_ushort v27, v[28:29], off
	s_nop 0
	global_load_ushort v28, v[32:33], off
	v_sub_u32_e32 v24, 0x3000, v18
	v_cndmask_b32_e64 v24, v24, 0, s[8:9]
	v_ashrrev_i32_e32 v25, 31, v24
	v_lshl_add_u64 v[24:25], v[24:25], 1, s[2:3]
	global_load_ushort v24, v[24:25], off
	s_nop 0
	global_load_ushort v33, v[22:23], off offset:3072
	s_waitcnt vmcnt(6)
	v_lshlrev_b32_e32 v13, 16, v13
	s_mov_b32 s56, s39
	s_mov_b32 s57, s38
	s_mov_b32 s58, s19
	s_mov_b32 s59, s18
	s_waitcnt vmcnt(5)
	v_lshlrev_b32_e32 v25, 16, v34
	v_cndmask_b32_e64 v32, -v25, v25, s[6:7]
	s_waitcnt vmcnt(4)
	v_lshlrev_b32_e32 v25, 16, v26
	v_cndmask_b32_e64 v36, -v25, v25, s[4:5]
	s_waitcnt vmcnt(3)
	v_lshlrev_b32_e32 v25, 16, v27
	v_cndmask_b32_e64 v37, -v25, v25, s[0:1]
	v_add_co_u32_e64 v26, s[0:1], s61, v16
	s_waitcnt vmcnt(2)
	v_lshlrev_b32_e32 v25, 16, v28
	s_waitcnt vmcnt(1)
	v_lshlrev_b32_e32 v24, 16, v24
	v_addc_co_u32_e64 v27, s[0:1], 0, v17, s[0:1]
	v_cndmask_b32_e64 v35, -v25, v25, vcc
	v_cndmask_b32_e64 v34, -v24, v24, s[8:9]
	v_sub_u32_e32 v24, 0x2e00, v18
	v_cmp_eq_u32_e32 vcc, s62, v18
	v_sub_u32_e32 v28, 0x2c00, v18
	v_cmp_eq_u32_e64 s[0:1], s63, v18
	v_cndmask_b32_e64 v24, v24, 0, vcc
	v_ashrrev_i32_e32 v25, 31, v24
	v_cndmask_b32_e64 v28, v28, 0, s[0:1]
	v_ashrrev_i32_e32 v29, 31, v28
	v_lshl_add_u64 v[24:25], v[24:25], 1, s[2:3]
	v_lshl_add_u64 v[28:29], v[28:29], 1, s[2:3]
	global_load_ushort v38, v[24:25], off
	s_nop 0
	global_load_ushort v28, v[28:29], off
	v_sub_u32_e32 v24, 0x2a00, v18
	v_cmp_eq_u32_e64 s[4:5], s64, v18
	v_cmp_eq_u32_e64 s[6:7], s65, v18
	s_mov_b32 s62, s29
	v_cndmask_b32_e64 v24, v24, 0, s[4:5]
	v_ashrrev_i32_e32 v25, 31, v24
	v_lshl_add_u64 v[24:25], v[24:25], 1, s[2:3]
	global_load_ushort v29, v[24:25], off
	v_sub_u32_e32 v24, 0x2800, v18
	v_cndmask_b32_e64 v24, v24, 0, s[6:7]
	v_ashrrev_i32_e32 v25, 31, v24
	v_lshl_add_u64 v[24:25], v[24:25], 1, s[2:3]
	global_load_ushort v41, v[26:27], off offset:1024
	global_load_ushort v40, v[26:27], off offset:2048
	global_load_ushort v39, v[26:27], off offset:3072
	global_load_ushort v42, v[24:25], off
	v_sub_u32_e32 v26, 0x2600, v18
	s_mov_b32 s63, s28
	s_mov_b32 s61, s24
	s_waitcnt vmcnt(6)
	v_lshlrev_b32_e32 v24, 16, v38
	v_cndmask_b32_e64 v45, -v24, v24, vcc
	s_waitcnt vmcnt(5)
	v_lshlrev_b32_e32 v24, 16, v28
	v_cndmask_b32_e64 v44, -v24, v24, s[0:1]
	s_movk_i32 s0, 0xe600
	v_sub_u32_e32 v38, 0x2200, v18
	s_waitcnt vmcnt(4)
	v_lshlrev_b32_e32 v24, 16, v29
	v_cndmask_b32_e64 v43, -v24, v24, s[4:5]
	v_add_co_u32_e32 v24, vcc, s45, v16
	s_nop 1
	v_addc_co_u32_e32 v25, vcc, 0, v17, vcc
	v_cmp_eq_u32_e32 vcc, s0, v18
	s_movk_i32 s0, 0xe400
	s_nop 0
	v_cndmask_b32_e64 v26, v26, 0, vcc
	v_ashrrev_i32_e32 v27, 31, v26
	v_lshl_add_u64 v[26:27], v[26:27], 1, s[2:3]
	global_load_ushort v26, v[26:27], off
	s_waitcnt vmcnt(1)
	v_lshlrev_b32_e32 v27, 16, v42
	v_cndmask_b32_e64 v49, -v27, v27, s[6:7]
	s_waitcnt vmcnt(0)
	v_lshlrev_b32_e32 v26, 16, v26
	v_cndmask_b32_e64 v50, -v26, v26, vcc
	v_cmp_eq_u32_e32 vcc, s0, v18
	v_add_co_u32_e64 v28, s[0:1], s86, v16
	v_sub_u32_e32 v26, 0x2400, v18
	s_nop 0
	v_addc_co_u32_e64 v29, s[0:1], 0, v17, s[0:1]
	s_movk_i32 s0, 0xe200
	s_nop 0
	v_cmp_eq_u32_e64 s[8:9], s0, v18
	s_movk_i32 s0, 0xe000
	v_cmp_eq_u32_e64 s[6:7], s0, v18
	v_cndmask_b32_e64 v46, v38, 0, s[8:9]
	v_sub_u32_e32 v38, 0x2000, v18
	s_movk_i32 s0, 0xde00
	v_cndmask_b32_e64 v52, v38, 0, s[6:7]
	v_sub_u32_e32 v38, 0x1e00, v18
	v_cmp_eq_u32_e64 s[4:5], s0, v18
	s_movk_i32 s0, 0xdc00
	v_cndmask_b32_e64 v26, v26, 0, vcc
	v_cndmask_b32_e64 v54, v38, 0, s[4:5]
	v_sub_u32_e32 v38, 0x1c00, v18
	v_cmp_eq_u32_e64 s[0:1], s0, v18
	v_ashrrev_i32_e32 v27, 31, v26
	v_ashrrev_i32_e32 v47, 31, v46
	v_cndmask_b32_e64 v56, v38, 0, s[0:1]
	v_lshl_add_u64 v[26:27], v[26:27], 1, s[2:3]
	v_lshl_add_u64 v[46:47], v[46:47], 1, s[2:3]
	v_ashrrev_i32_e32 v53, 31, v52
	v_ashrrev_i32_e32 v55, 31, v54
	v_ashrrev_i32_e32 v57, 31, v56
	v_lshl_add_u64 v[52:53], v[52:53], 1, s[2:3]
	v_lshl_add_u64 v[54:55], v[54:55], 1, s[2:3]
	v_lshl_add_u64 v[56:57], v[56:57], 1, s[2:3]
	global_load_ushort v38, v[26:27], off
	global_load_ushort v42, v[46:47], off
	s_nop 0
	global_load_ushort v46, v[52:53], off
	global_load_ushort v47, v[54:55], off
	global_load_ushort v48, v[56:57], off
	v_sub_u32_e32 v26, 0x1a00, v18
	v_cndmask_b32_e64 v26, v26, 0, s[10:11]
	v_ashrrev_i32_e32 v27, 31, v26
	v_lshl_add_u64 v[26:27], v[26:27], 1, s[2:3]
	global_load_ushort v26, v[26:27], off
	s_nop 0
	global_load_ushort v53, v[28:29], off offset:1024
	global_load_ushort v51, v[28:29], off offset:2048
	s_waitcnt vmcnt(7)
	v_lshlrev_b32_e32 v27, 16, v38
	v_cndmask_b32_e64 v61, -v27, v27, vcc
	s_waitcnt vmcnt(6)
	v_lshlrev_b32_e32 v27, 16, v42
	v_cndmask_b32_e64 v63, -v27, v27, s[8:9]
	s_waitcnt vmcnt(5)
	v_lshlrev_b32_e32 v27, 16, v46
	v_cndmask_b32_e64 v90, -v27, v27, s[6:7]
	s_waitcnt vmcnt(4)
	v_lshlrev_b32_e32 v27, 16, v47
	v_cndmask_b32_e64 v59, -v27, v27, s[4:5]
	s_waitcnt vmcnt(3)
	v_lshlrev_b32_e32 v27, 16, v48
	v_cndmask_b32_e64 v57, -v27, v27, s[0:1]
	s_movk_i32 s0, 0xd800
	v_sub_u32_e32 v38, 0x1800, v18
	v_cmp_eq_u32_e64 s[8:9], s0, v18
	s_movk_i32 s0, 0xd600
	s_waitcnt vmcnt(2)
	v_lshlrev_b32_e32 v26, 16, v26
	v_cndmask_b32_e64 v46, v38, 0, s[8:9]
	v_sub_u32_e32 v38, 0x1600, v18
	v_cmp_eq_u32_e64 s[6:7], s0, v18
	s_movk_i32 s0, 0xd400
	v_cndmask_b32_e64 v55, -v26, v26, s[10:11]
	v_add_co_u32_e32 v26, vcc, s88, v16
	v_cndmask_b32_e64 v64, v38, 0, s[6:7]
	v_sub_u32_e32 v38, 0x1400, v18
	v_cmp_eq_u32_e64 s[4:5], s0, v18
	s_movk_i32 s0, 0xd200
	v_addc_co_u32_e32 v27, vcc, 0, v17, vcc
	v_cndmask_b32_e64 v66, v38, 0, s[4:5]
	v_sub_u32_e32 v38, 0x1200, v18
	v_cmp_eq_u32_e64 s[0:1], s0, v18
	s_movk_i32 s10, 0xd000
	v_cmp_eq_u32_e32 vcc, s10, v18
	v_cndmask_b32_e64 v68, v38, 0, s[0:1]
	v_sub_u32_e32 v38, 0x1000, v18
	v_ashrrev_i32_e32 v47, 31, v46
	v_cndmask_b32_e64 v70, v38, 0, vcc
	v_lshl_add_u64 v[46:47], v[46:47], 1, s[2:3]
	v_ashrrev_i32_e32 v65, 31, v64
	v_ashrrev_i32_e32 v67, 31, v66
	v_ashrrev_i32_e32 v69, 31, v68
	v_ashrrev_i32_e32 v71, 31, v70
	s_movk_i32 s10, 0xce00
	v_lshl_add_u64 v[64:65], v[64:65], 1, s[2:3]
	v_lshl_add_u64 v[66:67], v[66:67], 1, s[2:3]
	v_lshl_add_u64 v[68:69], v[68:69], 1, s[2:3]
	v_lshl_add_u64 v[70:71], v[70:71], 1, s[2:3]
	global_load_ushort v38, v[46:47], off
	global_load_ushort v42, v[64:65], off
	global_load_ushort v48, v[66:67], off
	global_load_ushort v52, v[68:69], off
	global_load_ushort v54, v[70:71], off
	v_sub_u32_e32 v46, 0xe00, v18
	v_cmp_eq_u32_e64 s[12:13], s10, v18
	s_movk_i32 s10, 0xcc00
	v_cmp_eq_u32_e64 s[10:11], s10, v18
	v_cndmask_b32_e64 v46, v46, 0, s[12:13]
	v_ashrrev_i32_e32 v47, 31, v46
	v_lshl_add_u64 v[46:47], v[46:47], 1, s[2:3]
	global_load_ushort v56, v[46:47], off
	v_sub_u32_e32 v46, 0xc00, v18
	v_cndmask_b32_e64 v46, v46, 0, s[10:11]
	v_ashrrev_i32_e32 v47, 31, v46
	v_lshl_add_u64 v[46:47], v[46:47], 1, s[2:3]
	global_load_ushort v46, v[46:47], off
	s_nop 0
	global_load_ushort v91, v[28:29], off offset:3072
	s_waitcnt vmcnt(7)
	v_lshlrev_b32_e32 v28, 16, v38
	v_cndmask_b32_e64 v97, -v28, v28, s[8:9]
	s_waitcnt vmcnt(6)
	v_lshlrev_b32_e32 v28, 16, v42
	v_cndmask_b32_e64 v96, -v28, v28, s[6:7]
	s_waitcnt vmcnt(5)
	v_lshlrev_b32_e32 v28, 16, v48
	v_cndmask_b32_e64 v94, -v28, v28, s[4:5]
	s_waitcnt vmcnt(4)
	v_lshlrev_b32_e32 v28, 16, v52
	v_cndmask_b32_e64 v93, -v28, v28, s[0:1]
	s_waitcnt vmcnt(3)
	v_lshlrev_b32_e32 v28, 16, v54
	v_cndmask_b32_e64 v92, -v28, v28, vcc
	s_movk_i32 s0, 0xca00
	v_cmp_eq_u32_e64 s[0:1], s0, v18
	s_waitcnt vmcnt(2)
	v_lshlrev_b32_e32 v28, 16, v56
	v_cndmask_b32_e64 v95, -v28, v28, s[12:13]
	v_sub_u32_e32 v28, 0xa00, v18
	v_cndmask_b32_e64 v28, v28, 0, s[0:1]
	v_ashrrev_i32_e32 v29, 31, v28
	v_lshl_add_u64 v[28:29], v[28:29], 1, s[2:3]
	global_load_ushort v38, v[28:29], off
	s_waitcnt vmcnt(2)
	v_lshlrev_b32_e32 v28, 16, v46
	v_cndmask_b32_e64 v106, -v28, v28, s[10:11]
	v_add_co_u32_e32 v28, vcc, s90, v16
	s_movk_i32 s4, 0xc400
	s_nop 0
	v_addc_co_u32_e32 v29, vcc, 0, v17, vcc
	v_sub_u32_e32 v42, 0x400, v18
	v_cmp_eq_u32_e32 vcc, s4, v18
	s_movk_i32 s4, 0xc800
	v_cmp_eq_u32_e64 s[4:5], s4, v18
	v_cndmask_b32_e64 v46, v42, 0, vcc
	v_sub_u32_e32 v42, 0x800, v18
	v_ashrrev_i32_e32 v47, 31, v46
	v_cndmask_b32_e64 v64, v42, 0, s[4:5]
	v_lshl_add_u64 v[46:47], v[46:47], 1, s[2:3]
	v_ashrrev_i32_e32 v65, 31, v64
	v_lshl_add_u64 v[64:65], v[64:65], 1, s[2:3]
	global_load_ushort v42, v[46:47], off
	s_nop 0
	global_load_ushort v46, v[64:65], off
	global_load_ushort v110, v[28:29], off
	global_load_ushort v112, v[28:29], off offset:1024
	global_load_ushort v114, v[28:29], off offset:2048
	global_load_ushort v116, v[28:29], off offset:3072
	s_mov_b32 s10, 0x3f74fa0b
	s_mov_b32 s11, 0xbe94a031
	s_mov_b32 s80, s11
	s_mov_b32 s81, s10
	v_add_f32_e32 v52, v15, v13
	s_mov_b32 s12, 0x3e94a031
	s_mov_b32 s13, 0xbf74fa0b
	s_mov_b32 s64, s13
	s_mov_b32 s65, s12
	s_mov_b32 s8, 0x3e47c5c2
	s_mov_b32 s9, 0xbf7b14be
	s_mov_b32 s30, s9
	s_mov_b32 s31, s8
	s_mov_b32 s6, 0x3f7b14be
	s_mov_b32 s7, 0xbe47c5c2
	s_mov_b32 s6, s9
	s_waitcnt vmcnt(6)
	v_lshlrev_b32_e32 v28, 16, v38
	v_cndmask_b32_e64 v108, -v28, v28, s[0:1]
	s_movk_i32 s0, 0xc600
	v_sub_u32_e32 v28, 0x600, v18
	v_sub_u32_e32 v38, 0x200, v18
	s_waitcnt vmcnt(4)
	v_lshlrev_b32_e32 v29, 16, v46
	v_cndmask_b32_e64 v111, -v29, v29, s[4:5]
	v_cmp_eq_u32_e64 s[4:5], s0, v18
	s_movk_i32 s0, 0xc200
	v_cmp_eq_u32_e64 s[0:1], s0, v18
	v_cndmask_b32_e64 v28, v28, 0, s[4:5]
	v_ashrrev_i32_e32 v29, 31, v28
	v_cndmask_b32_e64 v46, v38, 0, s[0:1]
	v_lshl_add_u64 v[28:29], v[28:29], 1, s[2:3]
	v_ashrrev_i32_e32 v47, 31, v46
	v_lshl_add_u64 v[46:47], v[46:47], 1, s[2:3]
	global_load_ushort v18, v[16:17], off
	s_nop 0
	global_load_ushort v28, v[28:29], off
	s_nop 0
	global_load_ushort v29, v[16:17], off offset:1024
	s_nop 0
	global_load_ushort v17, v[16:17], off offset:2048
	s_nop 0
	global_load_ushort v38, v[46:47], off
	global_load_ushort v56, v[20:21], off offset:1024
	global_load_ushort v58, v[20:21], off offset:2048
	global_load_ushort v60, v[20:21], off offset:3072
	global_load_ushort v62, v[24:25], off offset:-4096
	global_load_ushort v98, v[24:25], off
	global_load_ushort v48, v[20:21], off offset:-4096
	global_load_ushort v64, v[22:23], off offset:1024
	global_load_ushort v68, v[22:23], off offset:2048
	s_nop 0
	global_load_ushort v21, v[20:21], off
	v_lshlrev_b32_e32 v22, 16, v42
	v_cndmask_b32_e64 v115, -v22, v22, vcc
	v_pk_mul_f32 v[22:23], v[14:15], s[78:79] op_sel_hi:[0,1] neg_lo:[1,0]
	s_mov_b64 vcc, s[66:67]
	s_mov_b32 s66, s71
	s_mov_b32 s67, s70
	s_mov_b32 s2, 0x3f7ec46d
	s_mov_b32 s3, 0xbdc8bd36
	s_waitcnt vmcnt(13)
	v_lshlrev_b32_e32 v16, 16, v18
	s_waitcnt vmcnt(12)
	v_lshlrev_b32_e32 v18, 16, v28
	s_waitcnt vmcnt(11)
	v_lshlrev_b32_e32 v20, 16, v29
	s_waitcnt vmcnt(10)
	v_lshlrev_b32_e32 v17, 16, v17
	v_add_f32_e32 v20, v31, v20
	v_pk_fma_f32 v[28:29], v[10:11], s[68:69], v[22:23] op_sel_hi:[0,1,1]
	v_add_f32_e32 v22, v30, v17
	v_pk_mul_f32 v[30:31], v[14:15], s[66:67] op_sel_hi:[0,1] neg_lo:[1,0]
	v_pk_fma_f32 v[46:47], v[10:11], s[70:71], v[30:31] op_sel_hi:[0,1,1]
	v_pk_mul_f32 v[30:31], v[14:15], s[80:81] op_sel_hi:[0,1] neg_lo:[1,0]
	v_pk_fma_f32 v[88:89], v[10:11], s[10:11], v[30:31] op_sel_hi:[0,1,1]
	s_waitcnt vmcnt(3)
	v_lshlrev_b32_e32 v13, 16, v48
	v_pk_mul_f32 v[30:31], v[14:15], s[52:53] op_sel_hi:[0,1] neg_lo:[1,0]
	v_add_f32_e32 v16, v19, v16
	v_cndmask_b32_e64 v113, -v18, v18, s[4:5]
	v_pk_mul_f32 v[18:19], v[14:15], s[40:41] op_sel_hi:[0,1] neg_lo:[1,0]
	v_add_f32_e32 v54, v32, v13
	v_pk_fma_f32 v[66:67], v[10:11], s[94:95], v[30:31] op_sel_hi:[0,1,1]
	s_waitcnt vmcnt(2)
	v_lshlrev_b32_e32 v13, 16, v64
	v_pk_mul_f32 v[30:31], v[14:15], s[50:51] op_sel_hi:[0,1] neg_lo:[1,0]
	s_waitcnt vmcnt(1)
	v_lshlrev_b32_e32 v15, 16, v68
	v_lshlrev_b32_e32 v17, 16, v38
	v_add_f32_e32 v32, v36, v13
	global_load_ushort v13, v[24:25], off offset:1024
	v_add_f32_e32 v38, v37, v15
	global_load_ushort v15, v[24:25], off offset:2048
	v_lshlrev_b32_e32 v23, 16, v33
	s_waitcnt vmcnt(2)
	v_lshlrev_b32_e32 v21, 16, v21
	v_add_f32_e32 v42, v35, v23
	global_load_ushort v23, v[24:25], off offset:3072
	global_load_ushort v33, v[26:27], off
	v_add_f32_e32 v48, v34, v21
	v_lshlrev_b32_e32 v21, 16, v56
	v_add_f32_e32 v56, v45, v21
	global_load_ushort v21, v[26:27], off offset:-4096
	s_mov_b32 s68, s83
	s_mov_b32 s69, s82
	s_mov_b32 s70, s23
	s_mov_b32 s71, s22
	v_pk_fma_f32 v[64:65], v[10:11], s[20:21], v[30:31] op_sel_hi:[0,1,1]
	s_mov_b32 s94, s75
	s_mov_b32 s95, s74
	s_mov_b32 s4, 0x3dc8bd36
	s_mov_b32 s5, 0xbf7ec46d
	s_mov_b32 s34, s5
	s_mov_b32 s35, s4
	s_mov_b32 s2, s5
	v_cndmask_b32_e64 v17, -v17, v17, s[0:1]
	s_mov_b32 s0, s3
	s_mov_b32 s1, s5
	s_mov_b32 s10, s13
	s_mov_b32 s20, s23
	v_pk_fma_f32 v[18:19], v[10:11], s[46:47], v[18:19] op_sel_hi:[0,1,1]
	s_waitcnt vmcnt(4)
	v_lshlrev_b32_e32 v13, 16, v13
	s_waitcnt vmcnt(3)
	v_pk_mul_f32 v[24:25], v[14:15], s[56:57] op_sel_hi:[0,1] neg_lo:[1,0]
	v_pk_fma_f32 v[76:77], v[10:11], s[38:39], v[24:25] op_sel_hi:[0,1,1]
	v_pk_mul_f32 v[24:25], v[14:15], s[62:63] op_sel_hi:[0,1] neg_lo:[1,0]
	v_pk_fma_f32 v[82:83], v[10:11], s[28:29], v[24:25] op_sel_hi:[0,1,1]
	v_lshlrev_b32_e32 v24, 16, v58
	v_add_f32_e32 v58, v44, v24
	v_pk_mul_f32 v[24:25], v[14:15], s[68:69] op_sel_hi:[0,1] neg_lo:[1,0]
	v_pk_fma_f32 v[84:85], v[10:11], s[82:83], v[24:25] op_sel_hi:[0,1,1]
	v_lshlrev_b32_e32 v24, 16, v60
	v_add_f32_e32 v60, v43, v24
	v_pk_mul_f32 v[24:25], v[14:15], s[70:71] op_sel_hi:[0,1] neg_lo:[1,0]
	v_pk_fma_f32 v[86:87], v[10:11], s[22:23], v[24:25] op_sel_hi:[0,1,1]
	v_lshlrev_b32_e32 v24, 16, v62
	v_add_f32_e32 v62, v49, v24
	v_pk_mul_f32 v[24:25], v[14:15], s[58:59] op_sel_hi:[0,1] neg_lo:[1,0]
	v_pk_fma_f32 v[80:81], v[10:11], s[18:19], v[24:25] op_sel_hi:[0,1,1]
	v_lshlrev_b32_e32 v24, 16, v41
	v_add_f32_e32 v50, v50, v24
	v_pk_mul_f32 v[24:25], v[14:15], s[64:65] op_sel_hi:[0,1] neg_lo:[1,0]
	v_pk_fma_f32 v[78:79], v[10:11], s[12:13], v[24:25] op_sel_hi:[0,1,1]
	v_lshlrev_b32_e32 v25, 16, v39
	v_add_f32_e32 v44, v63, v25
	global_load_ushort v25, v[26:27], off offset:1024
	global_load_ushort v39, v[26:27], off offset:2048
	v_lshlrev_b32_e32 v24, 16, v40
	global_load_ushort v40, v[26:27], off offset:3072
	v_pk_mul_f32 v[30:31], v[14:15], s[60:61] op_sel_hi:[0,1] neg_lo:[1,0]
	v_pk_fma_f32 v[68:69], v[10:11], s[24:25], v[30:31] op_sel_hi:[0,1,1]
	v_pk_mul_f32 v[30:31], v[14:15], s[94:95] op_sel_hi:[0,1] neg_lo:[1,0]
	v_pk_fma_f32 v[74:75], v[10:11], s[74:75], v[30:31] op_sel_hi:[0,1,1]
	v_pk_mul_f32 v[30:31], v[14:15], s[30:31] op_sel_hi:[0,1] neg_lo:[1,0]
	v_pk_fma_f32 v[70:71], v[10:11], s[8:9], v[30:31] op_sel_hi:[0,1,1]
	v_pk_mul_f32 v[30:31], v[14:15], s[34:35] op_sel_hi:[0,1] neg_lo:[1,0]
	v_pk_fma_f32 v[72:73], v[10:11], s[4:5], v[30:31] op_sel_hi:[0,1,1]
	v_lshlrev_b32_e32 v30, 16, v98
	v_pk_mul_f32 v[34:35], v[14:15], s[36:37] op_sel_hi:[0,1] neg_lo:[1,0]
	v_add_f32_e32 v30, v90, v30
	v_pk_fma_f32 v[34:35], v[10:11], s[76:77], v[34:35] op_sel_hi:[0,1,1]
	v_pk_mul_f32 v[36:37], v[34:35], v[30:31] op_sel_hi:[1,0]
	v_pk_mul_f32 v[30:31], v[14:15], s[2:3] op_sel_hi:[0,1] neg_lo:[1,0]
	v_add_f32_e32 v26, v59, v13
	v_pk_fma_f32 v[30:31], v[10:11], s[0:1], v[30:31] op_sel_hi:[0,1,1]
	v_lshlrev_b32_e32 v13, 16, v15
	s_mov_b32 s4, s7
	s_mov_b32 s5, s9
	v_pk_mul_f32 v[34:35], v[14:15], s[6:7] op_sel_hi:[0,1] neg_lo:[1,0]
	v_pk_mul_f32 v[26:27], v[30:31], v[26:27] op_sel_hi:[1,0]
	v_add_f32_e32 v30, v57, v13
	v_pk_fma_f32 v[34:35], v[10:11], s[4:5], v[34:35] op_sel_hi:[0,1,1]
	v_pk_mul_f32 v[98:99], v[34:35], v[30:31] op_sel_hi:[1,0]
	s_waitcnt vmcnt(5)
	v_lshlrev_b32_e32 v13, 16, v23
	s_mov_b32 s8, s11
	s_mov_b32 s9, s13
	v_pk_mul_f32 v[34:35], v[14:15], s[10:11] op_sel_hi:[0,1] neg_lo:[1,0]
	v_add_f32_e32 v30, v55, v13
	v_pk_fma_f32 v[34:35], v[10:11], s[8:9], v[34:35] op_sel_hi:[0,1,1]
	v_pk_mul_f32 v[100:101], v[34:35], v[30:31] op_sel_hi:[1,0]
	s_waitcnt vmcnt(3)
	v_lshlrev_b32_e32 v13, 16, v21
	s_mov_b32 s12, s17
	s_mov_b32 s13, s19
	v_pk_mul_f32 v[34:35], v[14:15], s[16:17] op_sel_hi:[0,1] neg_lo:[1,0]
	v_add_f32_e32 v30, v97, v13
	v_pk_fma_f32 v[34:35], v[10:11], s[12:13], v[34:35] op_sel_hi:[0,1,1]
	v_pk_mul_f32 v[102:103], v[34:35], v[30:31] op_sel_hi:[1,0]
	v_lshlrev_b32_e32 v13, 16, v53
	s_mov_b32 s18, s21
	s_mov_b32 s19, s23
	v_pk_mul_f32 v[34:35], v[14:15], s[20:21] op_sel_hi:[0,1] neg_lo:[1,0]
	v_add_f32_e32 v30, v96, v13
	v_pk_fma_f32 v[34:35], v[10:11], s[18:19], v[34:35] op_sel_hi:[0,1,1]
	s_mov_b32 s24, s83
	v_pk_mul_f32 v[96:97], v[34:35], v[30:31] op_sel_hi:[1,0]
	v_lshlrev_b32_e32 v13, 16, v51
	s_mov_b32 s22, s25
	s_mov_b32 s23, s83
	v_pk_mul_f32 v[34:35], v[14:15], s[24:25] op_sel_hi:[0,1] neg_lo:[1,0]
	v_add_f32_e32 v30, v94, v13
	v_pk_fma_f32 v[34:35], v[10:11], s[22:23], v[34:35] op_sel_hi:[0,1,1]
	s_mov_b32 s28, s29
	s_mov_b32 s29, s75
	v_pk_mul_f32 v[104:105], v[34:35], v[30:31] op_sel_hi:[1,0]
	v_lshlrev_b32_e32 v13, 16, v91
	v_pk_mul_f32 v[34:35], v[14:15], s[28:29] op_sel_hi:[0,1] neg_lo:[1,0]
	v_add_f32_e32 v30, v93, v13
	v_pk_fma_f32 v[34:35], v[10:11], s[26:27], v[34:35] op_sel_hi:[0,1,1]
	v_pk_mul_f32 v[90:91], v[34:35], v[30:31] op_sel_hi:[1,0]
	v_lshlrev_b32_e32 v13, 16, v33
	v_pk_mul_f32 v[34:35], v[14:15], s[38:39] op_sel_hi:[0,0] neg_lo:[1,0]
	s_mov_b32 s38, s39
	v_add_f32_e32 v30, v92, v13
	v_pk_fma_f32 v[34:35], v[10:11], s[38:39], v[34:35] op_sel_hi:[0,0,1] neg_lo:[0,0,1] neg_hi:[0,0,1]
	v_pk_mul_f32 v[92:93], v[34:35], v[30:31] op_sel_hi:[1,0]
	v_pk_mul_f32 v[34:35], v[14:15], s[26:27] op_sel_hi:[0,1] neg_lo:[1,0]
	v_pk_fma_f32 v[34:35], v[10:11], s[28:29], v[34:35] op_sel_hi:[0,1,1]
	v_add_f32_e32 v24, v61, v24
	s_waitcnt vmcnt(2)
	v_lshlrev_b32_e32 v13, 16, v25
	v_add_f32_e32 v30, v95, v13
	v_pk_mul_f32 v[94:95], v[34:35], v[30:31] op_sel_hi:[1,0]
	s_waitcnt vmcnt(1)
	v_lshlrev_b32_e32 v13, 16, v39
	v_pk_mul_f32 v[34:35], v[14:15], s[22:23] op_sel_hi:[0,1] neg_lo:[1,0]
	v_add_f32_e32 v30, v106, v13
	v_pk_fma_f32 v[34:35], v[10:11], s[24:25], v[34:35] op_sel_hi:[0,1,1]
	v_pk_mul_f32 v[106:107], v[34:35], v[30:31] op_sel_hi:[1,0]
	s_waitcnt vmcnt(0)
	v_lshlrev_b32_e32 v13, 16, v40
	v_pk_mul_f32 v[34:35], v[14:15], s[18:19] op_sel_hi:[0,1] neg_lo:[1,0]
	v_add_f32_e32 v30, v108, v13
	v_pk_fma_f32 v[34:35], v[10:11], s[20:21], v[34:35] op_sel_hi:[0,1,1]
	v_pk_mul_f32 v[108:109], v[34:35], v[30:31] op_sel_hi:[1,0]
	v_lshlrev_b32_e32 v13, 16, v110
	v_pk_mul_f32 v[34:35], v[14:15], s[12:13] op_sel_hi:[0,1] neg_lo:[1,0]
	v_add_f32_e32 v30, v111, v13
	v_pk_fma_f32 v[34:35], v[10:11], s[16:17], v[34:35] op_sel_hi:[0,1,1]
	v_pk_mul_f32 v[110:111], v[34:35], v[30:31] op_sel_hi:[1,0]
	v_lshlrev_b32_e32 v13, 16, v112
	v_pk_mul_f32 v[34:35], v[14:15], s[8:9] op_sel_hi:[0,1] neg_lo:[1,0]
	v_add_f32_e32 v30, v113, v13
	v_pk_fma_f32 v[34:35], v[10:11], s[10:11], v[34:35] op_sel_hi:[0,1,1]
	v_pk_mul_f32 v[112:113], v[34:35], v[30:31] op_sel_hi:[1,0]
	v_lshlrev_b32_e32 v13, 16, v114
	v_pk_mul_f32 v[34:35], v[14:15], s[4:5] op_sel_hi:[0,1] neg_lo:[1,0]
	v_add_f32_e32 v30, v115, v13
	v_pk_fma_f32 v[34:35], v[10:11], s[6:7], v[34:35] op_sel_hi:[0,1,1]
	v_lshlrev_b32_e32 v13, 16, v116
	v_pk_mul_f32 v[14:15], v[14:15], s[0:1] op_sel_hi:[0,1] neg_lo:[1,0]
	v_pk_mul_f32 v[114:115], v[34:35], v[30:31] op_sel_hi:[1,0]
	v_add_f32_e32 v30, v17, v13
	v_pk_fma_f32 v[14:15], v[10:11], s[2:3], v[14:15] op_sel_hi:[0,1,1]
	v_pk_mul_f32 v[116:117], v[14:15], v[30:31] op_sel_hi:[1,0]
	v_mov_b32_e32 v13, v174
	v_mov_b32_e32 v10, v164
	v_mov_b32_e32 v30, v166
	v_mov_b32_e32 v10, v168
	v_mov_b32_e32 v34, v170
	v_mov_b32_e32 v17, v172
	s_nop 0
	v_pk_fma_f32 v[126:127], v[18:19], v[16:17], v[36:37] op_sel_hi:[1,0,1]
	v_pk_fma_f32 v[36:37], v[18:19], v[16:17], v[36:37] op_sel_hi:[1,0,1] neg_lo:[0,0,1] neg_hi:[0,0,1]
	v_pk_fma_f32 v[18:19], v[28:29], v[20:21], v[26:27] op_sel_hi:[1,0,1] neg_lo:[0,0,1] neg_hi:[0,0,1]
	v_pk_fma_f32 v[16:17], v[28:29], v[20:21], v[26:27] op_sel_hi:[1,0,1]
	v_pk_mul_f32 v[20:21], v[18:19], v[124:125] op_sel:[1,0] op_sel_hi:[0,0] neg_lo:[1,1] neg_hi:[0,1]
	s_nop 0
	v_pk_fma_f32 v[40:41], v[18:19], v[118:119], v[20:21] op_sel_hi:[1,0,1]
	v_pk_fma_f32 v[20:21], v[46:47], v[22:23], v[98:99] op_sel_hi:[1,0,1] neg_lo:[0,0,1] neg_hi:[0,0,1]
	v_pk_fma_f32 v[18:19], v[46:47], v[22:23], v[98:99] op_sel_hi:[1,0,1]
	v_pk_mul_f32 v[22:23], v[20:21], v[34:35] op_sel:[1,0] op_sel_hi:[0,0] neg_lo:[1,1] neg_hi:[0,1]
	s_nop 0
	v_pk_fma_f32 v[46:47], v[20:21], v[30:31], v[22:23] op_sel_hi:[1,0,1]
	v_pk_fma_f32 v[22:23], v[88:89], v[52:53], v[100:101] op_sel_hi:[1,0,1] neg_lo:[0,0,1] neg_hi:[0,0,1]
	v_pk_fma_f32 v[20:21], v[88:89], v[52:53], v[100:101] op_sel_hi:[1,0,1]
	v_pk_mul_f32 v[26:27], v[22:23], v[122:123] op_sel:[1,0] op_sel_hi:[0,0] neg_lo:[1,1] neg_hi:[0,1]
	s_nop 0
	v_pk_fma_f32 v[52:53], v[22:23], v[120:121], v[26:27] op_sel_hi:[1,0,1]
	v_pk_fma_f32 v[26:27], v[66:67], v[54:55], v[102:103] op_sel_hi:[1,0,1] neg_lo:[0,0,1] neg_hi:[0,0,1]
	v_pk_fma_f32 v[22:23], v[66:67], v[54:55], v[102:103] op_sel_hi:[1,0,1]
	v_pk_mul_f32 v[28:29], v[26:27], v[10:11] op_sel:[1,0] op_sel_hi:[0,0] neg_lo:[1,1] neg_hi:[0,1]
	s_nop 0
	v_pk_fma_f32 v[54:55], v[26:27], v[10:11], v[28:29] op_sel_hi:[1,0,1]
	v_pk_fma_f32 v[28:29], v[64:65], v[32:33], v[96:97] op_sel_hi:[1,0,1] neg_lo:[0,0,1] neg_hi:[0,0,1]
	v_pk_fma_f32 v[26:27], v[64:65], v[32:33], v[96:97] op_sel_hi:[1,0,1]
	v_pk_mul_f32 v[32:33], v[28:29], v[122:123] op_sel_hi:[1,0]
	s_nop 0
	v_pk_fma_f32 v[64:65], v[28:29], v[120:121], v[32:33] op_sel:[1,0,0] op_sel_hi:[0,0,1] neg_lo:[1,1,0] neg_hi:[0,1,0]
	v_pk_fma_f32 v[32:33], v[68:69], v[38:39], v[104:105] op_sel_hi:[1,0,1] neg_lo:[0,0,1] neg_hi:[0,0,1]
	v_pk_fma_f32 v[28:29], v[68:69], v[38:39], v[104:105] op_sel_hi:[1,0,1]
	v_pk_mul_f32 v[38:39], v[32:33], v[34:35] op_sel_hi:[1,0]
	s_nop 0
	v_pk_fma_f32 v[66:67], v[32:33], v[30:31], v[38:39] op_sel:[1,0,0] op_sel_hi:[0,0,1] neg_lo:[1,1,0] neg_hi:[0,1,0]
	v_pk_fma_f32 v[38:39], v[74:75], v[42:43], v[90:91] op_sel_hi:[1,0,1] neg_lo:[0,0,1] neg_hi:[0,0,1]
	v_pk_fma_f32 v[32:33], v[74:75], v[42:43], v[90:91] op_sel_hi:[1,0,1]
	v_pk_mul_f32 v[42:43], v[38:39], v[124:125] op_sel_hi:[1,0]
	s_nop 0
	v_pk_fma_f32 v[68:69], v[38:39], v[118:119], v[42:43] op_sel:[1,0,0] op_sel_hi:[0,0,1] neg_lo:[1,1,0] neg_hi:[0,1,0]
	v_pk_fma_f32 v[38:39], v[76:77], v[48:49], v[92:93] op_sel_hi:[1,0,1]
	v_pk_fma_f32 v[42:43], v[76:77], v[48:49], v[92:93] op_sel_hi:[1,0,1] neg_lo:[0,0,1] neg_hi:[0,0,1]
	v_pk_fma_f32 v[48:49], v[82:83], v[56:57], v[94:95] op_sel_hi:[1,0,1] neg_lo:[0,0,1] neg_hi:[0,0,1]
	v_xor_b32_e32 v75, 0x80000000, v42
	v_mov_b32_e32 v74, v43
	v_pk_fma_f32 v[42:43], v[82:83], v[56:57], v[94:95] op_sel_hi:[1,0,1]
	v_pk_mul_f32 v[56:57], v[48:49], v[124:125] op_sel_hi:[1,0] neg_lo:[0,1] neg_hi:[0,1]
	v_xor_b32_e32 v76, 0x80000000, v49
	v_mov_b32_e32 v77, v48
	v_pk_fma_f32 v[48:49], v[84:85], v[58:59], v[106:107] op_sel_hi:[1,0,1]
	v_pk_fma_f32 v[58:59], v[84:85], v[58:59], v[106:107] op_sel_hi:[1,0,1] neg_lo:[0,0,1] neg_hi:[0,0,1]
	v_pk_fma_f32 v[56:57], v[76:77], v[118:119], v[56:57] op_sel_hi:[1,0,1] neg_lo:[0,1,0] neg_hi:[0,1,0]
	v_pk_mul_f32 v[76:77], v[58:59], v[34:35] op_sel_hi:[1,0] neg_lo:[0,1] neg_hi:[0,1]
	s_nop 0
	v_pk_fma_f32 v[58:59], v[58:59], v[30:31], v[76:77] op_sel:[1,0,0] op_sel_hi:[0,0,1] neg_lo:[1,1,0] neg_hi:[0,1,0]
	v_pk_fma_f32 v[76:77], v[86:87], v[60:61], v[108:109] op_sel_hi:[1,0,1]
	v_pk_fma_f32 v[60:61], v[86:87], v[60:61], v[108:109] op_sel_hi:[1,0,1] neg_lo:[0,0,1] neg_hi:[0,0,1]
	s_nop 0
	v_pk_mul_f32 v[82:83], v[60:61], v[122:123] op_sel_hi:[1,0] neg_lo:[0,1] neg_hi:[0,1]
	s_nop 0
	v_pk_fma_f32 v[60:61], v[60:61], v[120:121], v[82:83] op_sel:[1,0,0] op_sel_hi:[0,0,1] neg_lo:[1,1,0] neg_hi:[0,1,0]
	v_pk_fma_f32 v[82:83], v[80:81], v[62:63], v[110:111] op_sel_hi:[1,0,1]
	v_pk_fma_f32 v[62:63], v[80:81], v[62:63], v[110:111] op_sel_hi:[1,0,1] neg_lo:[0,0,1] neg_hi:[0,0,1]
	v_pk_add_f32 v[84:85], v[126:127], v[38:39] neg_lo:[0,1] neg_hi:[0,1]
	v_pk_mul_f32 v[80:81], v[62:63], v[10:11] op_sel:[1,0] op_sel_hi:[0,0] neg_lo:[1,1] neg_hi:[0,1]
	s_nop 0
	v_pk_fma_f32 v[62:63], v[62:63], v[10:11], v[80:81] op_sel_hi:[1,0,1] neg_lo:[0,1,0] neg_hi:[0,1,0]
	v_pk_fma_f32 v[80:81], v[78:79], v[50:51], v[112:113] op_sel_hi:[1,0,1]
	v_pk_fma_f32 v[50:51], v[78:79], v[50:51], v[112:113] op_sel_hi:[1,0,1] neg_lo:[0,0,1] neg_hi:[0,0,1]
	s_nop 0
	v_pk_mul_f32 v[78:79], v[50:51], v[122:123] op_sel:[1,0] op_sel_hi:[0,0] neg_lo:[1,1] neg_hi:[0,1]
	s_nop 0
	v_pk_fma_f32 v[50:51], v[50:51], v[120:121], v[78:79] op_sel_hi:[1,0,1] neg_lo:[0,1,0] neg_hi:[0,1,0]
	v_pk_fma_f32 v[78:79], v[70:71], v[24:25], v[114:115] op_sel_hi:[1,0,1]
	v_pk_fma_f32 v[24:25], v[70:71], v[24:25], v[114:115] op_sel_hi:[1,0,1] neg_lo:[0,0,1] neg_hi:[0,0,1]
	s_nop 0
	v_pk_mul_f32 v[70:71], v[24:25], v[34:35] op_sel:[1,0] op_sel_hi:[0,0] neg_lo:[1,1] neg_hi:[0,1]
	s_nop 0
	v_pk_fma_f32 v[70:71], v[24:25], v[30:31], v[70:71] op_sel_hi:[1,0,1] neg_lo:[0,1,0] neg_hi:[0,1,0]
	v_pk_fma_f32 v[24:25], v[72:73], v[44:45], v[116:117] op_sel_hi:[1,0,1]
	v_pk_fma_f32 v[44:45], v[72:73], v[44:45], v[116:117] op_sel_hi:[1,0,1] neg_lo:[0,0,1] neg_hi:[0,0,1]
	s_nop 0
	v_pk_mul_f32 v[72:73], v[44:45], v[124:125] op_sel:[1,0] op_sel_hi:[0,0] neg_lo:[1,1] neg_hi:[0,1]
	s_nop 0
	v_pk_fma_f32 v[72:73], v[118:119], v[44:45], v[72:73] op_sel_hi:[0,1,1] neg_lo:[1,0,0] neg_hi:[1,0,0]
	v_pk_add_f32 v[44:45], v[126:127], v[38:39]
	v_pk_add_f32 v[38:39], v[16:17], v[42:43]
	v_pk_add_f32 v[16:17], v[16:17], v[42:43] neg_lo:[0,1] neg_hi:[0,1]
	s_nop 0
	v_pk_mul_f32 v[42:43], v[16:17], v[34:35] op_sel:[1,0] op_sel_hi:[0,0] neg_lo:[1,1] neg_hi:[0,1]
	s_nop 0
	v_pk_fma_f32 v[42:43], v[16:17], v[30:31], v[42:43] op_sel_hi:[1,0,1]
	v_pk_add_f32 v[16:17], v[18:19], v[48:49]
	v_pk_add_f32 v[18:19], v[18:19], v[48:49] neg_lo:[0,1] neg_hi:[0,1]
	s_nop 0
	v_pk_mul_f32 v[48:49], v[18:19], v[10:11] op_sel:[1,0] op_sel_hi:[0,0] neg_lo:[1,1] neg_hi:[0,1]
	s_nop 0
	v_pk_fma_f32 v[18:19], v[18:19], v[10:11], v[48:49] op_sel_hi:[1,0,1]
	v_pk_add_f32 v[48:49], v[20:21], v[76:77]
	v_pk_add_f32 v[20:21], v[20:21], v[76:77] neg_lo:[0,1] neg_hi:[0,1]
	s_nop 0
	v_pk_mul_f32 v[76:77], v[20:21], v[34:35] op_sel_hi:[1,0]
	v_xor_b32_e32 v86, 0x80000000, v21
	v_mov_b32_e32 v87, v20
	v_pk_add_f32 v[20:21], v[22:23], v[82:83]
	v_pk_add_f32 v[22:23], v[22:23], v[82:83] neg_lo:[0,1] neg_hi:[0,1]
	v_pk_fma_f32 v[76:77], v[86:87], v[30:31], v[76:77] op_sel_hi:[1,0,1] neg_lo:[0,1,0] neg_hi:[0,1,0]
	v_xor_b32_e32 v83, 0x80000000, v22
	v_mov_b32_e32 v82, v23
	v_pk_add_f32 v[22:23], v[26:27], v[80:81]
	v_pk_add_f32 v[26:27], v[26:27], v[80:81] neg_lo:[0,1] neg_hi:[0,1]
	s_nop 0
	v_pk_mul_f32 v[80:81], v[26:27], v[34:35] op_sel_hi:[1,0] neg_lo:[0,1] neg_hi:[0,1]
	s_nop 0
	v_pk_fma_f32 v[26:27], v[30:31], v[26:27], v[80:81] op_sel:[0,1,0] op_sel_hi:[0,0,1] neg_lo:[1,1,0] neg_hi:[1,0,0]
	v_pk_add_f32 v[80:81], v[28:29], v[78:79]
	v_pk_add_f32 v[28:29], v[28:29], v[78:79] neg_lo:[0,1] neg_hi:[0,1]
	v_pk_add_f32 v[86:87], v[44:45], v[20:21] neg_lo:[0,1] neg_hi:[0,1]
	v_pk_mul_f32 v[78:79], v[10:11], v[28:29] op_sel:[0,1] op_sel_hi:[0,0] neg_lo:[1,1] neg_hi:[1,0]
	v_pk_fma_f32 v[78:79], v[28:29], v[10:11], v[78:79] op_sel_hi:[1,0,1] neg_lo:[0,1,0] neg_hi:[0,1,0]
	v_pk_add_f32 v[28:29], v[32:33], v[24:25]
	v_pk_add_f32 v[24:25], v[32:33], v[24:25] neg_lo:[0,1] neg_hi:[0,1]
	s_nop 0
	v_pk_mul_f32 v[32:33], v[34:35], v[24:25] op_sel:[0,1] op_sel_hi:[0,0] neg_lo:[1,1] neg_hi:[1,0]
	v_pk_fma_f32 v[32:33], v[30:31], v[24:25], v[32:33] op_sel_hi:[0,1,1] neg_lo:[1,0,0] neg_hi:[1,0,0]
	v_pk_add_f32 v[24:25], v[44:45], v[20:21]
	v_pk_add_f32 v[20:21], v[38:39], v[22:23]
	v_pk_add_f32 v[22:23], v[38:39], v[22:23] neg_lo:[0,1] neg_hi:[0,1]
	s_nop 0
	v_pk_mul_f32 v[38:39], v[10:11], v[22:23] op_sel:[0,1] op_sel_hi:[0,0] neg_lo:[1,1] neg_hi:[1,0]
	v_pk_fma_f32 v[22:23], v[22:23], v[10:11], v[38:39] op_sel_hi:[1,0,1]
	v_pk_add_f32 v[38:39], v[16:17], v[80:81]
	v_pk_add_f32 v[16:17], v[16:17], v[80:81] neg_lo:[0,1] neg_hi:[0,1]
	s_nop 0
	v_xor_b32_e32 v81, 0x80000000, v16
	v_mov_b32_e32 v80, v17
	v_pk_add_f32 v[16:17], v[48:49], v[28:29]
	v_pk_add_f32 v[28:29], v[48:49], v[28:29] neg_lo:[0,1] neg_hi:[0,1]
	s_nop 0
	v_pk_mul_f32 v[44:45], v[10:11], v[28:29] op_sel:[0,1] op_sel_hi:[0,0] neg_lo:[1,1] neg_hi:[1,0]
	v_pk_fma_f32 v[48:49], v[10:11], v[28:29], v[44:45] op_sel_hi:[0,1,1] neg_lo:[1,0,0] neg_hi:[1,0,0]
	v_pk_add_f32 v[28:29], v[24:25], v[38:39]
	v_pk_add_f32 v[24:25], v[24:25], v[38:39] neg_lo:[0,1] neg_hi:[0,1]
	v_pk_add_f32 v[38:39], v[20:21], v[16:17]
	v_pk_add_f32 v[16:17], v[20:21], v[16:17] neg_lo:[0,1] neg_hi:[0,1]
	v_pk_add_f32 v[88:89], v[28:29], v[38:39]
	v_pk_add_f32 v[44:45], v[24:25], v[16:17] op_sel:[0,1] op_sel_hi:[1,0] neg_hi:[0,1]
	v_pk_add_f32 v[20:21], v[24:25], v[16:17] op_sel:[0,1] op_sel_hi:[1,0] neg_lo:[0,1]
	v_pk_add_f32 v[24:25], v[22:23], v[48:49]
	v_pk_add_f32 v[22:23], v[22:23], v[48:49] neg_lo:[0,1] neg_hi:[0,1]
	v_pk_add_f32 v[16:17], v[86:87], v[80:81]
	v_pk_add_f32 v[80:81], v[86:87], v[80:81] neg_lo:[0,1] neg_hi:[0,1]
	v_pk_add_f32 v[28:29], v[28:29], v[38:39] neg_lo:[0,1] neg_hi:[0,1]
	v_pk_add_f32 v[86:87], v[16:17], v[24:25]
	v_pk_add_f32 v[24:25], v[16:17], v[24:25] neg_lo:[0,1] neg_hi:[0,1]
	v_pk_add_f32 v[38:39], v[80:81], v[22:23] op_sel:[0,1] op_sel_hi:[1,0] neg_hi:[0,1]
	v_pk_add_f32 v[16:17], v[80:81], v[22:23] op_sel:[0,1] op_sel_hi:[1,0] neg_lo:[0,1]
	v_pk_add_f32 v[48:49], v[42:43], v[26:27]
	v_pk_add_f32 v[26:27], v[42:43], v[26:27] neg_lo:[0,1] neg_hi:[0,1]
	v_pk_add_f32 v[22:23], v[84:85], v[82:83]
	v_pk_mul_f32 v[42:43], v[10:11], v[26:27] op_sel:[0,1] op_sel_hi:[0,0] neg_lo:[1,1] neg_hi:[1,0]
	v_pk_fma_f32 v[26:27], v[10:11], v[26:27], v[42:43] op_sel_hi:[0,1,1]
	v_pk_add_f32 v[42:43], v[18:19], v[78:79]
	v_pk_add_f32 v[18:19], v[18:19], v[78:79] neg_lo:[0,1] neg_hi:[0,1]
	v_pk_add_f32 v[80:81], v[84:85], v[82:83] neg_lo:[0,1] neg_hi:[0,1]
	v_xor_b32_e32 v79, 0x80000000, v18
	v_mov_b32_e32 v78, v19
	v_pk_add_f32 v[18:19], v[76:77], v[32:33]
	v_pk_add_f32 v[32:33], v[76:77], v[32:33] neg_lo:[0,1] neg_hi:[0,1]
	s_nop 0
	v_pk_mul_f32 v[76:77], v[10:11], v[32:33] op_sel:[0,1] op_sel_hi:[0,0] neg_lo:[1,1] neg_hi:[1,0]
	v_pk_fma_f32 v[76:77], v[10:11], v[32:33], v[76:77] op_sel_hi:[0,1,1] neg_lo:[1,0,0] neg_hi:[1,0,0]
	v_pk_add_f32 v[32:33], v[22:23], v[42:43]
	v_pk_add_f32 v[22:23], v[22:23], v[42:43] neg_lo:[0,1] neg_hi:[0,1]
	v_pk_add_f32 v[42:43], v[48:49], v[18:19]
	v_pk_add_f32 v[18:19], v[48:49], v[18:19] neg_lo:[0,1] neg_hi:[0,1]
	v_pk_add_f32 v[84:85], v[32:33], v[42:43]
	v_pk_add_f32 v[32:33], v[32:33], v[42:43] neg_lo:[0,1] neg_hi:[0,1]
	v_pk_add_f32 v[42:43], v[26:27], v[76:77]
	v_pk_add_f32 v[26:27], v[26:27], v[76:77] neg_lo:[0,1] neg_hi:[0,1]
	v_xor_b32_e32 v83, 0x80000000, v18
	v_mov_b32_e32 v82, v19
	v_pk_add_f32 v[18:19], v[80:81], v[78:79]
	v_pk_add_f32 v[78:79], v[80:81], v[78:79] neg_lo:[0,1] neg_hi:[0,1]
	v_xor_b32_e32 v77, 0x80000000, v26
	v_mov_b32_e32 v76, v27
	v_pk_add_f32 v[80:81], v[18:19], v[42:43]
	v_pk_add_f32 v[26:27], v[18:19], v[42:43] neg_lo:[0,1] neg_hi:[0,1]
	v_pk_add_f32 v[42:43], v[78:79], v[76:77]
	v_pk_add_f32 v[18:19], v[78:79], v[76:77] neg_lo:[0,1] neg_hi:[0,1]
	v_pk_add_f32 v[76:77], v[36:37], v[74:75]
	v_pk_add_f32 v[74:75], v[36:37], v[74:75] neg_lo:[0,1] neg_hi:[0,1]
	v_pk_add_f32 v[36:37], v[40:41], v[56:57]
	v_pk_add_f32 v[40:41], v[40:41], v[56:57] neg_lo:[0,1] neg_hi:[0,1]
	v_pk_add_f32 v[48:49], v[22:23], v[82:83]
	v_pk_mul_f32 v[56:57], v[34:35], v[40:41] op_sel:[0,1] op_sel_hi:[0,0] neg_lo:[1,1] neg_hi:[1,0]
	v_pk_fma_f32 v[40:41], v[30:31], v[40:41], v[56:57] op_sel_hi:[0,1,1]
	v_pk_add_f32 v[56:57], v[46:47], v[58:59]
	v_pk_add_f32 v[46:47], v[46:47], v[58:59] neg_lo:[0,1] neg_hi:[0,1]
	v_pk_add_f32 v[22:23], v[22:23], v[82:83] neg_lo:[0,1] neg_hi:[0,1]
	v_pk_mul_f32 v[58:59], v[10:11], v[46:47] op_sel:[0,1] op_sel_hi:[0,0] neg_lo:[1,1] neg_hi:[1,0]
	v_pk_fma_f32 v[58:59], v[10:11], v[46:47], v[58:59] op_sel_hi:[0,1,1]
	v_pk_add_f32 v[46:47], v[52:53], v[60:61]
	v_pk_add_f32 v[52:53], v[52:53], v[60:61] neg_lo:[0,1] neg_hi:[0,1]
	s_nop 0
	v_pk_mul_f32 v[60:61], v[30:31], v[52:53] op_sel:[0,1] op_sel_hi:[0,0] neg_lo:[1,1] neg_hi:[1,0]
	v_pk_fma_f32 v[60:61], v[34:35], v[52:53], v[60:61] op_sel_hi:[0,1,1]
	v_pk_add_f32 v[52:53], v[54:55], v[62:63]
	v_pk_add_f32 v[54:55], v[54:55], v[62:63] neg_lo:[0,1] neg_hi:[0,1]
	s_nop 0
	v_xor_b32_e32 v63, 0x80000000, v54
	v_mov_b32_e32 v62, v55
	v_pk_add_f32 v[54:55], v[64:65], v[50:51]
	v_pk_add_f32 v[50:51], v[64:65], v[50:51] neg_lo:[0,1] neg_hi:[0,1]
	s_nop 0
	v_pk_mul_f32 v[64:65], v[30:31], v[50:51] op_sel:[0,1] op_sel_hi:[0,0] neg_lo:[1,1] neg_hi:[1,0]
	v_pk_fma_f32 v[50:51], v[34:35], v[50:51], v[64:65] op_sel_hi:[0,1,1] neg_lo:[1,0,0] neg_hi:[1,0,0]
	v_pk_add_f32 v[64:65], v[66:67], v[70:71]
	v_pk_add_f32 v[66:67], v[66:67], v[70:71] neg_lo:[0,1] neg_hi:[0,1]
	s_nop 0
	v_pk_mul_f32 v[70:71], v[10:11], v[66:67] op_sel:[0,1] op_sel_hi:[0,0] neg_lo:[1,1] neg_hi:[1,0]
	v_pk_fma_f32 v[66:67], v[10:11], v[66:67], v[70:71] op_sel_hi:[0,1,1] neg_lo:[1,0,0] neg_hi:[1,0,0]
	v_pk_add_f32 v[70:71], v[68:69], v[72:73]
	v_pk_add_f32 v[68:69], v[68:69], v[72:73] neg_lo:[0,1] neg_hi:[0,1]
	s_nop 0
	v_pk_mul_f32 v[34:35], v[34:35], v[68:69] op_sel:[0,1] op_sel_hi:[0,0] neg_lo:[1,1] neg_hi:[1,0]
	v_pk_fma_f32 v[34:35], v[30:31], v[68:69], v[34:35] op_sel_hi:[0,1,1] neg_lo:[1,0,0] neg_hi:[1,0,0]
	v_pk_add_f32 v[30:31], v[76:77], v[52:53]
	v_pk_add_f32 v[68:69], v[76:77], v[52:53] neg_lo:[0,1] neg_hi:[0,1]
	v_pk_add_f32 v[52:53], v[54:55], v[36:37]
	v_pk_add_f32 v[36:37], v[36:37], v[54:55] neg_lo:[0,1] neg_hi:[0,1]
	s_nop 0
	v_pk_mul_f32 v[54:55], v[10:11], v[36:37] op_sel:[0,1] op_sel_hi:[0,0] neg_lo:[1,1] neg_hi:[1,0]
	v_pk_fma_f32 v[54:55], v[10:11], v[36:37], v[54:55] op_sel_hi:[0,1,1]
	v_pk_add_f32 v[36:37], v[56:57], v[64:65]
	v_pk_add_f32 v[56:57], v[56:57], v[64:65] neg_lo:[0,1] neg_hi:[0,1]
	s_nop 0
	v_xor_b32_e32 v65, 0x80000000, v56
	v_mov_b32_e32 v64, v57
	v_pk_add_f32 v[56:57], v[46:47], v[70:71]
	v_pk_add_f32 v[46:47], v[46:47], v[70:71] neg_lo:[0,1] neg_hi:[0,1]
	s_nop 0
	v_pk_mul_f32 v[70:71], v[10:11], v[46:47] op_sel:[0,1] op_sel_hi:[0,0] neg_lo:[1,1] neg_hi:[1,0]
	v_pk_fma_f32 v[46:47], v[10:11], v[46:47], v[70:71] op_sel_hi:[0,1,1] neg_lo:[1,0,0] neg_hi:[1,0,0]
	v_pk_add_f32 v[70:71], v[30:31], v[36:37]
	v_pk_add_f32 v[30:31], v[30:31], v[36:37] neg_lo:[0,1] neg_hi:[0,1]
	v_pk_add_f32 v[36:37], v[52:53], v[56:57]
	v_pk_add_f32 v[52:53], v[52:53], v[56:57] neg_lo:[0,1] neg_hi:[0,1]
	v_pk_add_f32 v[72:73], v[70:71], v[36:37]
	v_xor_b32_e32 v57, 0x80000000, v52
	v_mov_b32_e32 v56, v53
	v_pk_add_f32 v[52:53], v[70:71], v[36:37] neg_lo:[0,1] neg_hi:[0,1]
	v_pk_add_f32 v[70:71], v[30:31], v[56:57]
	v_pk_add_f32 v[36:37], v[30:31], v[56:57] neg_lo:[0,1] neg_hi:[0,1]
	v_pk_add_f32 v[30:31], v[68:69], v[64:65]
	v_pk_add_f32 v[56:57], v[68:69], v[64:65] neg_lo:[0,1] neg_hi:[0,1]
	v_pk_add_f32 v[64:65], v[54:55], v[46:47]
	v_pk_add_f32 v[46:47], v[54:55], v[46:47] neg_lo:[0,1] neg_hi:[0,1]
	v_pk_add_f32 v[68:69], v[30:31], v[64:65]
	v_xor_b32_e32 v55, 0x80000000, v46
	v_mov_b32_e32 v54, v47
	v_pk_add_f32 v[46:47], v[30:31], v[64:65] neg_lo:[0,1] neg_hi:[0,1]
	v_pk_add_f32 v[64:65], v[56:57], v[54:55]
	v_pk_add_f32 v[30:31], v[56:57], v[54:55] neg_lo:[0,1] neg_hi:[0,1]
	v_pk_add_f32 v[54:55], v[74:75], v[62:63]
	v_pk_add_f32 v[56:57], v[74:75], v[62:63] neg_lo:[0,1] neg_hi:[0,1]
	v_pk_add_f32 v[62:63], v[50:51], v[40:41]
	v_pk_add_f32 v[40:41], v[40:41], v[50:51] neg_lo:[0,1] neg_hi:[0,1]
	s_nop 0
	v_pk_mul_f32 v[50:51], v[10:11], v[40:41] op_sel:[0,1] op_sel_hi:[0,0] neg_lo:[1,1] neg_hi:[1,0]
	v_pk_fma_f32 v[50:51], v[10:11], v[40:41], v[50:51] op_sel_hi:[0,1,1]
	v_pk_add_f32 v[40:41], v[58:59], v[66:67]
	v_pk_add_f32 v[58:59], v[58:59], v[66:67] neg_lo:[0,1] neg_hi:[0,1]
	s_nop 0
	v_xor_b32_e32 v67, 0x80000000, v58
	v_mov_b32_e32 v66, v59
	v_pk_add_f32 v[58:59], v[60:61], v[34:35]
	v_pk_add_f32 v[34:35], v[60:61], v[34:35] neg_lo:[0,1] neg_hi:[0,1]
	s_nop 0
	v_pk_mul_f32 v[60:61], v[10:11], v[34:35] op_sel:[0,1] op_sel_hi:[0,0] neg_lo:[1,1] neg_hi:[1,0]
	v_pk_fma_f32 v[34:35], v[10:11], v[34:35], v[60:61] op_sel_hi:[0,1,1] neg_lo:[1,0,0] neg_hi:[1,0,0]
	v_pk_add_f32 v[60:61], v[54:55], v[40:41]
	v_pk_add_f32 v[40:41], v[54:55], v[40:41] neg_lo:[0,1] neg_hi:[0,1]
	v_pk_add_f32 v[54:55], v[62:63], v[58:59]
	v_pk_add_f32 v[58:59], v[62:63], v[58:59] neg_lo:[0,1] neg_hi:[0,1]
	v_lshl_add_u32 v10, v13, 3, 0
	v_xor_b32_e32 v63, 0x80000000, v58
	v_mov_b32_e32 v62, v59
	v_pk_add_f32 v[58:59], v[60:61], v[54:55]
	v_pk_add_f32 v[54:55], v[60:61], v[54:55] neg_lo:[0,1] neg_hi:[0,1]
	v_pk_add_f32 v[60:61], v[40:41], v[62:63]
	v_pk_add_f32 v[40:41], v[40:41], v[62:63] neg_lo:[0,1] neg_hi:[0,1]
	v_pk_add_f32 v[62:63], v[56:57], v[66:67]
	v_pk_add_f32 v[56:57], v[56:57], v[66:67] neg_lo:[0,1] neg_hi:[0,1]
	v_pk_add_f32 v[66:67], v[50:51], v[34:35]
	v_pk_add_f32 v[34:35], v[50:51], v[34:35] neg_lo:[0,1] neg_hi:[0,1]
	v_pk_add_f32 v[76:77], v[62:63], v[66:67]
	v_pk_add_f32 v[50:51], v[62:63], v[66:67] neg_lo:[0,1] neg_hi:[0,1]
	v_pk_add_f32 v[62:63], v[56:57], v[34:35] op_sel:[0,1] op_sel_hi:[1,0] neg_hi:[0,1]
	v_pk_add_f32 v[34:35], v[56:57], v[34:35] op_sel:[0,1] op_sel_hi:[1,0] neg_lo:[0,1]
	v_pk_mul_f32 v[56:57], v[88:89], s[14:15] op_sel:[1,0] neg_lo:[1,0]
	s_nop 0
	v_pk_fma_f32 v[56:57], v[88:89], s[42:43], v[56:57] op_sel_hi:[0,1,1]
	ds_write_b64 v10, v[56:57]
	v_pk_fma_f32 v[56:57], v[180:181], s[92:93], v[180:181] op_sel:[1,0,0] op_sel_hi:[0,1,1]
	v_pk_mul_f32 v[66:67], v[56:57], v[72:73] op_sel:[1,1] op_sel_hi:[0,1] neg_lo:[0,1]
	v_pk_fma_f32 v[66:67], v[56:57], v[72:73], v[66:67] op_sel_hi:[1,0,1]
	ds_write_b64 v10, v[66:67] offset:4224
	v_pk_mul_f32 v[66:67], v[180:181], v[56:57] op_sel:[1,1] op_sel_hi:[0,1] neg_lo:[0,1]
	v_pk_fma_f32 v[56:57], v[180:181], v[56:57], v[66:67] op_sel_hi:[1,0,1]
	s_nop 0
	v_pk_mul_f32 v[66:67], v[56:57], v[84:85] op_sel:[1,1] op_sel_hi:[0,1] neg_lo:[0,1]
	v_pk_fma_f32 v[66:67], v[56:57], v[84:85], v[66:67] op_sel_hi:[1,0,1]
	ds_write_b64 v10, v[66:67] offset:8448
	v_pk_mul_f32 v[66:67], v[180:181], v[56:57] op_sel:[1,1] op_sel_hi:[0,1] neg_lo:[0,1]
	v_pk_fma_f32 v[56:57], v[180:181], v[56:57], v[66:67] op_sel_hi:[1,0,1]
	s_nop 0
	v_pk_mul_f32 v[66:67], v[56:57], v[58:59] op_sel:[1,1] op_sel_hi:[0,1] neg_lo:[0,1]
	v_pk_fma_f32 v[58:59], v[56:57], v[58:59], v[66:67] op_sel_hi:[1,0,1]
	ds_write_b64 v10, v[58:59] offset:12672
	v_pk_mul_f32 v[58:59], v[180:181], v[56:57] op_sel:[1,1] op_sel_hi:[0,1] neg_lo:[0,1]
	v_pk_fma_f32 v[56:57], v[180:181], v[56:57], v[58:59] op_sel_hi:[1,0,1]
	s_nop 0
	v_pk_mul_f32 v[58:59], v[56:57], v[86:87] op_sel:[1,1] op_sel_hi:[0,1] neg_lo:[0,1]
	v_pk_fma_f32 v[58:59], v[56:57], v[86:87], v[58:59] op_sel_hi:[1,0,1]
	ds_write_b64 v10, v[58:59] offset:16896
	v_pk_mul_f32 v[58:59], v[180:181], v[56:57] op_sel:[1,1] op_sel_hi:[0,1] neg_lo:[0,1]
	v_pk_fma_f32 v[56:57], v[180:181], v[56:57], v[58:59] op_sel_hi:[1,0,1]
	s_nop 0
	v_pk_mul_f32 v[58:59], v[56:57], v[68:69] op_sel:[1,1] op_sel_hi:[0,1] neg_lo:[0,1]
	v_pk_fma_f32 v[58:59], v[56:57], v[68:69], v[58:59] op_sel_hi:[1,0,1]
	ds_write_b64 v10, v[58:59] offset:21120
	v_pk_mul_f32 v[58:59], v[180:181], v[56:57] op_sel:[1,1] op_sel_hi:[0,1] neg_lo:[0,1]
	v_pk_fma_f32 v[56:57], v[180:181], v[56:57], v[58:59] op_sel_hi:[1,0,1]
	s_nop 0
	v_pk_mul_f32 v[58:59], v[80:81], v[56:57] op_sel:[1,1] op_sel_hi:[1,0] neg_lo:[1,0]
	s_nop 0
	v_pk_fma_f32 v[58:59], v[80:81], v[56:57], v[58:59] op_sel_hi:[0,1,1]
	ds_write_b64 v10, v[58:59] offset:25344
	v_pk_mul_f32 v[58:59], v[180:181], v[56:57] op_sel:[1,1] op_sel_hi:[0,1] neg_lo:[0,1]
	v_pk_fma_f32 v[56:57], v[180:181], v[56:57], v[58:59] op_sel_hi:[1,0,1]
	s_nop 0
	v_pk_mul_f32 v[58:59], v[76:77], v[56:57] op_sel:[1,1] op_sel_hi:[1,0] neg_lo:[1,0]
	s_nop 0
	v_pk_fma_f32 v[58:59], v[76:77], v[56:57], v[58:59] op_sel_hi:[0,1,1]
	ds_write_b64 v10, v[58:59] offset:29568
	v_pk_mul_f32 v[58:59], v[180:181], v[56:57] op_sel:[1,1] op_sel_hi:[0,1] neg_lo:[0,1]
	v_pk_fma_f32 v[56:57], v[180:181], v[56:57], v[58:59] op_sel_hi:[1,0,1]
	s_nop 0
	v_pk_mul_f32 v[58:59], v[44:45], v[56:57] op_sel:[1,1] op_sel_hi:[1,0] neg_lo:[1,0]
	s_nop 0
	v_pk_fma_f32 v[44:45], v[44:45], v[56:57], v[58:59] op_sel_hi:[0,1,1]
	ds_write_b64 v10, v[44:45] offset:33792
	v_pk_mul_f32 v[44:45], v[180:181], v[56:57] op_sel:[1,1] op_sel_hi:[0,1] neg_lo:[0,1]
	v_pk_fma_f32 v[44:45], v[180:181], v[56:57], v[44:45] op_sel_hi:[1,0,1]
	s_nop 0
	v_pk_mul_f32 v[56:57], v[70:71], v[44:45] op_sel:[1,1] op_sel_hi:[1,0] neg_lo:[1,0]
	s_nop 0
	v_pk_fma_f32 v[56:57], v[70:71], v[44:45], v[56:57] op_sel_hi:[0,1,1]
	ds_write_b64 v10, v[56:57] offset:38016
	v_pk_mul_f32 v[56:57], v[180:181], v[44:45] op_sel:[1,1] op_sel_hi:[0,1] neg_lo:[0,1]
	v_pk_fma_f32 v[44:45], v[180:181], v[44:45], v[56:57] op_sel_hi:[1,0,1]
	s_nop 0
	v_pk_mul_f32 v[56:57], v[48:49], v[44:45] op_sel:[1,1] op_sel_hi:[1,0] neg_lo:[1,0]
	s_nop 0
	v_pk_fma_f32 v[48:49], v[48:49], v[44:45], v[56:57] op_sel_hi:[0,1,1]
	ds_write_b64 v10, v[48:49] offset:42240
	v_pk_mul_f32 v[48:49], v[180:181], v[44:45] op_sel:[1,1] op_sel_hi:[0,1] neg_lo:[0,1]
	v_pk_fma_f32 v[44:45], v[180:181], v[44:45], v[48:49] op_sel_hi:[1,0,1]
	s_nop 0
	v_pk_mul_f32 v[48:49], v[60:61], v[44:45] op_sel:[1,1] op_sel_hi:[1,0] neg_lo:[1,0]
	s_nop 0
	v_pk_fma_f32 v[48:49], v[60:61], v[44:45], v[48:49] op_sel_hi:[0,1,1]
	ds_write_b64 v10, v[48:49] offset:46464
	v_pk_mul_f32 v[48:49], v[180:181], v[44:45] op_sel:[1,1] op_sel_hi:[0,1] neg_lo:[0,1]
	v_pk_fma_f32 v[44:45], v[180:181], v[44:45], v[48:49] op_sel_hi:[1,0,1]
	s_nop 0
	v_pk_mul_f32 v[48:49], v[38:39], v[44:45] op_sel:[1,1] op_sel_hi:[1,0] neg_lo:[1,0]
	s_nop 0
	v_pk_fma_f32 v[38:39], v[38:39], v[44:45], v[48:49] op_sel_hi:[0,1,1]
	ds_write_b64 v10, v[38:39] offset:50688
	v_pk_mul_f32 v[38:39], v[180:181], v[44:45] op_sel:[1,1] op_sel_hi:[0,1] neg_lo:[0,1]
	v_pk_fma_f32 v[38:39], v[180:181], v[44:45], v[38:39] op_sel_hi:[1,0,1]
	s_nop 0
	v_pk_mul_f32 v[44:45], v[64:65], v[38:39] op_sel:[1,1] op_sel_hi:[1,0] neg_lo:[1,0]
	s_nop 0
	v_pk_fma_f32 v[44:45], v[64:65], v[38:39], v[44:45] op_sel_hi:[0,1,1]
	ds_write_b64 v10, v[44:45] offset:54912
	v_pk_mul_f32 v[44:45], v[180:181], v[38:39] op_sel:[1,1] op_sel_hi:[0,1] neg_lo:[0,1]
	v_pk_fma_f32 v[38:39], v[180:181], v[38:39], v[44:45] op_sel_hi:[1,0,1]
	s_nop 0
	v_pk_mul_f32 v[44:45], v[42:43], v[38:39] op_sel:[1,1] op_sel_hi:[1,0] neg_lo:[1,0]
	s_nop 0
	v_pk_fma_f32 v[42:43], v[42:43], v[38:39], v[44:45] op_sel_hi:[0,1,1]
	ds_write_b64 v10, v[42:43] offset:59136
	v_pk_mul_f32 v[42:43], v[180:181], v[38:39] op_sel:[1,1] op_sel_hi:[0,1] neg_lo:[0,1]
	v_pk_fma_f32 v[38:39], v[180:181], v[38:39], v[42:43] op_sel_hi:[1,0,1]
	s_nop 0
	v_pk_mul_f32 v[42:43], v[62:63], v[38:39] op_sel:[1,1] op_sel_hi:[1,0] neg_lo:[1,0]
	s_nop 0
	v_pk_fma_f32 v[42:43], v[62:63], v[38:39], v[42:43] op_sel_hi:[0,1,1]
	ds_write_b64 v10, v[42:43] offset:63360
	v_pk_mul_f32 v[42:43], v[180:181], v[38:39] op_sel:[1,1] op_sel_hi:[0,1] neg_lo:[0,1]
	v_pk_fma_f32 v[38:39], v[180:181], v[38:39], v[42:43] op_sel_hi:[1,0,1]
	s_nop 0
	v_pk_mul_f32 v[42:43], v[28:29], v[38:39] op_sel:[1,1] op_sel_hi:[1,0] neg_lo:[1,0]
	v_add_u32_e32 v13, 0x10800, v10
	v_pk_fma_f32 v[28:29], v[28:29], v[38:39], v[42:43] op_sel_hi:[0,1,1]
	ds_write_b64 v13, v[28:29]
	v_pk_mul_f32 v[28:29], v[180:181], v[38:39] op_sel:[1,1] op_sel_hi:[0,1] neg_lo:[0,1]
	v_pk_fma_f32 v[28:29], v[180:181], v[38:39], v[28:29] op_sel_hi:[1,0,1]
	s_nop 0
	v_pk_mul_f32 v[38:39], v[52:53], v[28:29] op_sel:[1,1] op_sel_hi:[1,0] neg_lo:[1,0]
	v_add_u32_e32 v13, 0x11880, v10
	v_pk_fma_f32 v[38:39], v[52:53], v[28:29], v[38:39] op_sel_hi:[0,1,1]
	ds_write_b64 v13, v[38:39]
	v_pk_mul_f32 v[38:39], v[180:181], v[28:29] op_sel:[1,1] op_sel_hi:[0,1] neg_lo:[0,1]
	v_pk_fma_f32 v[28:29], v[180:181], v[28:29], v[38:39] op_sel_hi:[1,0,1]
	s_nop 0
	v_pk_mul_f32 v[38:39], v[32:33], v[28:29] op_sel:[1,1] op_sel_hi:[1,0] neg_lo:[1,0]
	v_add_u32_e32 v13, 0x12900, v10
	v_pk_fma_f32 v[32:33], v[32:33], v[28:29], v[38:39] op_sel_hi:[0,1,1]
	ds_write_b64 v13, v[32:33]
	v_pk_mul_f32 v[32:33], v[180:181], v[28:29] op_sel:[1,1] op_sel_hi:[0,1] neg_lo:[0,1]
	v_pk_fma_f32 v[28:29], v[180:181], v[28:29], v[32:33] op_sel_hi:[1,0,1]
	s_nop 0
	v_pk_mul_f32 v[32:33], v[54:55], v[28:29] op_sel:[1,1] op_sel_hi:[1,0] neg_lo:[1,0]
	v_add_u32_e32 v13, 0x13980, v10
	v_pk_fma_f32 v[32:33], v[54:55], v[28:29], v[32:33] op_sel_hi:[0,1,1]
	ds_write_b64 v13, v[32:33]
	v_pk_mul_f32 v[32:33], v[180:181], v[28:29] op_sel:[1,1] op_sel_hi:[0,1] neg_lo:[0,1]
	v_pk_fma_f32 v[28:29], v[180:181], v[28:29], v[32:33] op_sel_hi:[1,0,1]
	s_nop 0
	v_pk_mul_f32 v[32:33], v[24:25], v[28:29] op_sel:[1,1] op_sel_hi:[1,0] neg_lo:[1,0]
	v_add_u32_e32 v13, 0x14a00, v10
	v_pk_fma_f32 v[24:25], v[24:25], v[28:29], v[32:33] op_sel_hi:[0,1,1]
	ds_write_b64 v13, v[24:25]
	v_pk_mul_f32 v[24:25], v[180:181], v[28:29] op_sel:[1,1] op_sel_hi:[0,1] neg_lo:[0,1]
	v_pk_fma_f32 v[24:25], v[180:181], v[28:29], v[24:25] op_sel_hi:[1,0,1]
	s_nop 0
	v_pk_mul_f32 v[28:29], v[46:47], v[24:25] op_sel:[1,1] op_sel_hi:[1,0] neg_lo:[1,0]
	v_add_u32_e32 v13, 0x15a80, v10
	v_pk_fma_f32 v[28:29], v[46:47], v[24:25], v[28:29] op_sel_hi:[0,1,1]
	ds_write_b64 v13, v[28:29]
	v_pk_mul_f32 v[28:29], v[180:181], v[24:25] op_sel:[1,1] op_sel_hi:[0,1] neg_lo:[0,1]
	v_pk_fma_f32 v[24:25], v[180:181], v[24:25], v[28:29] op_sel_hi:[1,0,1]
	s_nop 0
	v_pk_mul_f32 v[28:29], v[26:27], v[24:25] op_sel:[1,1] op_sel_hi:[1,0] neg_lo:[1,0]
	v_add_u32_e32 v13, 0x16b00, v10
	v_pk_fma_f32 v[26:27], v[26:27], v[24:25], v[28:29] op_sel_hi:[0,1,1]
	ds_write_b64 v13, v[26:27]
	v_pk_mul_f32 v[26:27], v[180:181], v[24:25] op_sel:[1,1] op_sel_hi:[0,1] neg_lo:[0,1]
	v_pk_fma_f32 v[24:25], v[180:181], v[24:25], v[26:27] op_sel_hi:[1,0,1]
	s_nop 0
	v_pk_mul_f32 v[26:27], v[50:51], v[24:25] op_sel:[1,1] op_sel_hi:[1,0] neg_lo:[1,0]
	v_add_u32_e32 v13, 0x17b80, v10
	v_pk_fma_f32 v[26:27], v[50:51], v[24:25], v[26:27] op_sel_hi:[0,1,1]
	ds_write_b64 v13, v[26:27]
	v_pk_mul_f32 v[26:27], v[180:181], v[24:25] op_sel:[1,1] op_sel_hi:[0,1] neg_lo:[0,1]
	v_pk_fma_f32 v[24:25], v[180:181], v[24:25], v[26:27] op_sel_hi:[1,0,1]
	s_nop 0
	v_pk_mul_f32 v[26:27], v[20:21], v[24:25] op_sel:[1,1] op_sel_hi:[1,0] neg_lo:[1,0]
	v_add_u32_e32 v13, 0x18c00, v10
	v_pk_fma_f32 v[20:21], v[20:21], v[24:25], v[26:27] op_sel_hi:[0,1,1]
	ds_write_b64 v13, v[20:21]
	v_pk_mul_f32 v[20:21], v[180:181], v[24:25] op_sel:[1,1] op_sel_hi:[0,1] neg_lo:[0,1]
	v_pk_fma_f32 v[20:21], v[180:181], v[24:25], v[20:21] op_sel_hi:[1,0,1]
	s_nop 0
	v_pk_mul_f32 v[24:25], v[36:37], v[20:21] op_sel:[1,1] op_sel_hi:[1,0] neg_lo:[1,0]
	v_add_u32_e32 v13, 0x19c80, v10
	v_pk_fma_f32 v[24:25], v[36:37], v[20:21], v[24:25] op_sel_hi:[0,1,1]
	ds_write_b64 v13, v[24:25]
	v_pk_mul_f32 v[24:25], v[180:181], v[20:21] op_sel:[1,1] op_sel_hi:[0,1] neg_lo:[0,1]
	v_pk_fma_f32 v[20:21], v[180:181], v[20:21], v[24:25] op_sel_hi:[1,0,1]
	s_nop 0
	v_pk_mul_f32 v[24:25], v[22:23], v[20:21] op_sel:[1,1] op_sel_hi:[1,0] neg_lo:[1,0]
	v_add_u32_e32 v13, 0x1ad00, v10
	v_pk_fma_f32 v[22:23], v[22:23], v[20:21], v[24:25] op_sel_hi:[0,1,1]
	ds_write_b64 v13, v[22:23]
	v_pk_mul_f32 v[22:23], v[180:181], v[20:21] op_sel:[1,1] op_sel_hi:[0,1] neg_lo:[0,1]
	v_pk_fma_f32 v[20:21], v[180:181], v[20:21], v[22:23] op_sel_hi:[1,0,1]
	s_nop 0
	v_pk_mul_f32 v[22:23], v[40:41], v[20:21] op_sel:[1,1] op_sel_hi:[1,0] neg_lo:[1,0]
	v_add_u32_e32 v13, 0x1bd80, v10
	v_pk_fma_f32 v[22:23], v[40:41], v[20:21], v[22:23] op_sel_hi:[0,1,1]
	ds_write_b64 v13, v[22:23]
	v_pk_mul_f32 v[22:23], v[180:181], v[20:21] op_sel:[1,1] op_sel_hi:[0,1] neg_lo:[0,1]
	v_pk_fma_f32 v[20:21], v[180:181], v[20:21], v[22:23] op_sel_hi:[1,0,1]
	s_nop 0
	v_pk_mul_f32 v[22:23], v[16:17], v[20:21] op_sel:[1,1] op_sel_hi:[1,0] neg_lo:[1,0]
	v_add_u32_e32 v13, 0x1ce00, v10
	v_pk_fma_f32 v[16:17], v[16:17], v[20:21], v[22:23] op_sel_hi:[0,1,1]
	ds_write_b64 v13, v[16:17]
	v_pk_mul_f32 v[16:17], v[180:181], v[20:21] op_sel:[1,1] op_sel_hi:[0,1] neg_lo:[0,1]
	v_pk_fma_f32 v[16:17], v[180:181], v[20:21], v[16:17] op_sel_hi:[1,0,1]
	s_nop 0
	v_pk_mul_f32 v[20:21], v[30:31], v[16:17] op_sel:[1,1] op_sel_hi:[1,0] neg_lo:[1,0]
	v_add_u32_e32 v13, 0x1de80, v10
	v_pk_fma_f32 v[20:21], v[30:31], v[16:17], v[20:21] op_sel_hi:[0,1,1]
	ds_write_b64 v13, v[20:21]
	v_pk_mul_f32 v[20:21], v[180:181], v[16:17] op_sel:[1,1] op_sel_hi:[0,1] neg_lo:[0,1]
	v_pk_fma_f32 v[16:17], v[180:181], v[16:17], v[20:21] op_sel_hi:[1,0,1]
	s_nop 0
	v_pk_mul_f32 v[20:21], v[18:19], v[16:17] op_sel:[1,1] op_sel_hi:[1,0] neg_lo:[1,0]
	v_add_u32_e32 v13, 0x1ef00, v10
	v_pk_fma_f32 v[18:19], v[18:19], v[16:17], v[20:21] op_sel_hi:[0,1,1]
	ds_write_b64 v13, v[18:19]
	v_pk_mul_f32 v[18:19], v[180:181], v[16:17] op_sel:[1,1] op_sel_hi:[0,1] neg_lo:[0,1]
	v_pk_fma_f32 v[14:15], v[180:181], v[16:17], v[18:19] op_sel_hi:[1,0,1]
	s_nop 0
	v_pk_mul_f32 v[16:17], v[34:35], v[14:15] op_sel:[1,1] op_sel_hi:[1,0] neg_lo:[1,0]
	v_add_u32_e32 v10, 0x1ff80, v10
	v_pk_fma_f32 v[14:15], v[34:35], v[14:15], v[16:17] op_sel_hi:[0,1,1]
	ds_write_b64 v10, v[14:15]
	v_mov_b32_e32 v10, v176
	v_mov_b32_e32 v13, v173
	s_waitcnt lgkmcnt(0)
	s_barrier
	v_mov_b32_e32 v14, v182
	v_xad_u32 v28, v13, 3, v10
	v_lshl_add_u32 v71, v28, 3, 0
	v_xad_u32 v28, v13, 4, v10
	v_lshl_add_u32 v70, v28, 3, 0
	v_xad_u32 v28, v13, 5, v10
	v_lshl_add_u32 v69, v28, 3, 0
	v_xad_u32 v28, v13, 6, v10
	v_lshl_add_u32 v68, v28, 3, 0
	v_xad_u32 v28, v13, 7, v10
	v_lshl_add_u32 v67, v28, 3, 0
	v_xad_u32 v28, v13, 8, v10
	v_lshl_add_u32 v28, v28, 3, 0
	v_add_u32_e32 v66, 0x800, v28
	v_xad_u32 v28, v13, 9, v10
	v_lshl_add_u32 v28, v28, 3, 0
	v_add_u32_e32 v65, 0x800, v28
	v_xad_u32 v28, v13, 10, v10
	v_lshl_add_u32 v28, v28, 3, 0
	v_add_u32_e32 v64, 0x800, v28
	v_xad_u32 v28, v13, 11, v10
	v_lshl_add_u32 v28, v28, 3, 0
	v_add_u32_e32 v16, v13, v10
	v_add_u32_e32 v63, 0x800, v28
	v_xad_u32 v28, v13, 12, v10
	v_mov_b32_e32 v15, v183
	v_lshl_add_u32 v74, v16, 3, 0
	v_lshl_add_u32 v28, v28, 3, 0
	ds_read2_b64 v[16:19], v74 offset1:16
	ds_read2_b64 v[38:41], v66 offset1:16
	v_add_u32_e32 v62, 0x800, v28
	v_xad_u32 v28, v13, 13, v10
	v_xad_u32 v20, v13, 1, v10
	v_lshl_add_u32 v28, v28, 3, 0
	v_lshl_add_u32 v73, v20, 3, 0
	v_xad_u32 v24, v13, 2, v10
	v_add_u32_e32 v61, 0x800, v28
	v_xad_u32 v28, v13, 14, v10
	v_xad_u32 v10, v13, 15, v10
	ds_read2_b64 v[20:23], v73 offset0:32 offset1:48
	ds_read2_b64 v[46:49], v65 offset0:32 offset1:48
	v_lshl_add_u32 v28, v28, 3, 0
	v_lshl_add_u32 v10, v10, 3, 0
	v_lshl_add_u32 v72, v24, 3, 0
	v_add_u32_e32 v60, 0x800, v28
	v_add_u32_e32 v13, 0x800, v10
	v_mov_b32_e32 v10, v164
	ds_read2_b64 v[24:27], v72 offset0:64 offset1:80
	ds_read2_b64 v[56:59], v71 offset0:96 offset1:112
	ds_read2_b64 v[76:79], v70 offset0:128 offset1:144
	ds_read2_b64 v[80:83], v69 offset0:160 offset1:176
	ds_read2_b64 v[84:87], v68 offset0:192 offset1:208
	ds_read2_b64 v[88:91], v67 offset0:224 offset1:240
	ds_read2_b64 v[52:55], v64 offset0:64 offset1:80
	ds_read2_b64 v[92:95], v63 offset0:96 offset1:112
	ds_read2_b64 v[96:99], v62 offset0:128 offset1:144
	ds_read2_b64 v[100:103], v61 offset0:160 offset1:176
	ds_read2_b64 v[104:107], v60 offset0:192 offset1:208
	ds_read2_b64 v[108:111], v13 offset0:224 offset1:240
	s_waitcnt lgkmcnt(14)
	v_pk_add_f32 v[112:113], v[16:17], v[38:39]
	v_pk_add_f32 v[38:39], v[16:17], v[38:39] neg_lo:[0,1] neg_hi:[0,1]
	v_pk_add_f32 v[16:17], v[18:19], v[40:41]
	v_pk_add_f32 v[18:19], v[18:19], v[40:41] neg_lo:[0,1] neg_hi:[0,1]
	v_mov_b32_e32 v28, v165
	v_mov_b32_e32 v30, v166
	v_mov_b32_e32 v32, v167
	v_mov_b32_e32 v10, v168
	v_mov_b32_e32 v36, v169
	v_mov_b32_e32 v34, v170
	v_mov_b32_e32 v44, v171
	v_mov_b32_e32 v29, v172
	v_pk_mul_f32 v[40:41], v[18:19], v[44:45] op_sel:[1,0] op_sel_hi:[0,0] neg_lo:[1,1] neg_hi:[0,1]
	s_nop 0
	v_pk_fma_f32 v[42:43], v[18:19], v[28:29], v[40:41] op_sel_hi:[1,0,1]
	s_waitcnt lgkmcnt(12)
	v_pk_add_f32 v[18:19], v[20:21], v[46:47]
	v_pk_add_f32 v[20:21], v[20:21], v[46:47] neg_lo:[0,1] neg_hi:[0,1]
	s_nop 0
	v_pk_mul_f32 v[40:41], v[20:21], v[34:35] op_sel:[1,0] op_sel_hi:[0,0] neg_lo:[1,1] neg_hi:[0,1]
	s_nop 0
	v_pk_fma_f32 v[46:47], v[20:21], v[30:31], v[40:41] op_sel_hi:[1,0,1]
	v_pk_add_f32 v[20:21], v[22:23], v[48:49]
	v_pk_add_f32 v[22:23], v[22:23], v[48:49] neg_lo:[0,1] neg_hi:[0,1]
	s_nop 0
	v_pk_mul_f32 v[40:41], v[22:23], v[36:37] op_sel:[1,0] op_sel_hi:[0,0] neg_lo:[1,1] neg_hi:[0,1]
	s_nop 0
	v_pk_fma_f32 v[50:51], v[22:23], v[32:33], v[40:41] op_sel_hi:[1,0,1]
	s_waitcnt lgkmcnt(5)
	v_pk_add_f32 v[22:23], v[24:25], v[52:53]
	v_pk_add_f32 v[24:25], v[24:25], v[52:53] neg_lo:[0,1] neg_hi:[0,1]
	s_nop 0
	v_pk_mul_f32 v[40:41], v[24:25], v[10:11] op_sel:[1,0] op_sel_hi:[0,0] neg_lo:[1,1] neg_hi:[0,1]
	s_nop 0
	v_pk_fma_f32 v[52:53], v[24:25], v[10:11], v[40:41] op_sel_hi:[1,0,1]
	v_pk_add_f32 v[24:25], v[26:27], v[54:55]
	v_pk_add_f32 v[26:27], v[26:27], v[54:55] neg_lo:[0,1] neg_hi:[0,1]
	s_nop 0
	v_pk_mul_f32 v[40:41], v[26:27], v[36:37] op_sel_hi:[1,0]
	s_nop 0
	v_pk_fma_f32 v[54:55], v[26:27], v[32:33], v[40:41] op_sel:[1,0,0] op_sel_hi:[0,0,1] neg_lo:[1,1,0] neg_hi:[0,1,0]
	s_waitcnt lgkmcnt(4)
	v_pk_add_f32 v[40:41], v[56:57], v[92:93] neg_lo:[0,1] neg_hi:[0,1]
	v_pk_add_f32 v[26:27], v[56:57], v[92:93]
	v_pk_mul_f32 v[48:49], v[40:41], v[34:35] op_sel_hi:[1,0]
	s_nop 0
	v_pk_fma_f32 v[56:57], v[40:41], v[30:31], v[48:49] op_sel:[1,0,0] op_sel_hi:[0,0,1] neg_lo:[1,1,0] neg_hi:[0,1,0]
	v_pk_add_f32 v[48:49], v[58:59], v[94:95] neg_lo:[0,1] neg_hi:[0,1]
	v_pk_add_f32 v[40:41], v[58:59], v[94:95]
	v_pk_mul_f32 v[58:59], v[48:49], v[44:45] op_sel_hi:[1,0]
	v_xor_b32_e32 v92, 0x80000000, v49
	v_mov_b32_e32 v93, v48
	s_waitcnt lgkmcnt(3)
	v_pk_add_f32 v[48:49], v[76:77], v[96:97]
	v_pk_add_f32 v[76:77], v[76:77], v[96:97] neg_lo:[0,1] neg_hi:[0,1]
	v_pk_fma_f32 v[58:59], v[92:93], v[28:29], v[58:59] op_sel_hi:[1,0,1] neg_lo:[0,1,0] neg_hi:[0,1,0]
	v_xor_b32_e32 v93, 0x80000000, v76
	v_mov_b32_e32 v92, v77
	v_pk_add_f32 v[76:77], v[78:79], v[98:99]
	v_pk_add_f32 v[78:79], v[78:79], v[98:99] neg_lo:[0,1] neg_hi:[0,1]
	s_nop 0
	v_pk_mul_f32 v[94:95], v[78:79], v[44:45] op_sel_hi:[1,0] neg_lo:[0,1] neg_hi:[0,1]
	s_nop 0
	v_pk_fma_f32 v[78:79], v[78:79], v[28:29], v[94:95] op_sel:[1,0,0] op_sel_hi:[0,0,1] neg_lo:[1,1,0] neg_hi:[0,1,0]
	s_waitcnt lgkmcnt(2)
	v_pk_add_f32 v[94:95], v[80:81], v[100:101]
	v_pk_add_f32 v[80:81], v[80:81], v[100:101] neg_lo:[0,1] neg_hi:[0,1]
	s_nop 0
	v_pk_mul_f32 v[96:97], v[80:81], v[34:35] op_sel_hi:[1,0] neg_lo:[0,1] neg_hi:[0,1]
	s_nop 0
	v_pk_fma_f32 v[80:81], v[80:81], v[30:31], v[96:97] op_sel:[1,0,0] op_sel_hi:[0,0,1] neg_lo:[1,1,0] neg_hi:[0,1,0]
	v_pk_add_f32 v[96:97], v[82:83], v[102:103]
	v_pk_add_f32 v[82:83], v[82:83], v[102:103] neg_lo:[0,1] neg_hi:[0,1]
	s_nop 0
	v_pk_mul_f32 v[98:99], v[82:83], v[36:37] op_sel_hi:[1,0] neg_lo:[0,1] neg_hi:[0,1]
	s_nop 0
	v_pk_fma_f32 v[82:83], v[82:83], v[32:33], v[98:99] op_sel:[1,0,0] op_sel_hi:[0,0,1] neg_lo:[1,1,0] neg_hi:[0,1,0]
	s_waitcnt lgkmcnt(1)
	v_pk_add_f32 v[98:99], v[84:85], v[104:105]
	v_pk_add_f32 v[84:85], v[84:85], v[104:105] neg_lo:[0,1] neg_hi:[0,1]
	s_nop 0
	v_pk_mul_f32 v[100:101], v[84:85], v[10:11] op_sel:[1,0] op_sel_hi:[0,0] neg_lo:[1,1] neg_hi:[0,1]
	s_nop 0
	v_pk_fma_f32 v[84:85], v[84:85], v[10:11], v[100:101] op_sel_hi:[1,0,1] neg_lo:[0,1,0] neg_hi:[0,1,0]
	v_pk_add_f32 v[100:101], v[86:87], v[106:107]
	v_pk_add_f32 v[86:87], v[86:87], v[106:107] neg_lo:[0,1] neg_hi:[0,1]
	s_nop 0
	v_pk_mul_f32 v[36:37], v[86:87], v[36:37] op_sel:[1,0] op_sel_hi:[0,0] neg_lo:[1,1] neg_hi:[0,1]
	s_nop 0
	v_pk_fma_f32 v[86:87], v[86:87], v[32:33], v[36:37] op_sel_hi:[1,0,1] neg_lo:[0,1,0] neg_hi:[0,1,0]
	s_waitcnt lgkmcnt(0)
	v_pk_add_f32 v[36:37], v[88:89], v[108:109] neg_lo:[0,1] neg_hi:[0,1]
	v_pk_add_f32 v[32:33], v[88:89], v[108:109]
	v_pk_mul_f32 v[88:89], v[36:37], v[34:35] op_sel:[1,0] op_sel_hi:[0,0] neg_lo:[1,1] neg_hi:[0,1]
	s_nop 0
	v_pk_fma_f32 v[88:89], v[36:37], v[30:31], v[88:89] op_sel_hi:[1,0,1] neg_lo:[0,1,0] neg_hi:[0,1,0]
	v_pk_add_f32 v[36:37], v[90:91], v[110:111]
	v_pk_add_f32 v[90:91], v[90:91], v[110:111] neg_lo:[0,1] neg_hi:[0,1]
	s_nop 0
	v_pk_mul_f32 v[44:45], v[90:91], v[44:45] op_sel:[1,0] op_sel_hi:[0,0] neg_lo:[1,1] neg_hi:[0,1]
	s_nop 0
	v_pk_fma_f32 v[90:91], v[90:91], v[28:29], v[44:45] op_sel_hi:[1,0,1] neg_lo:[0,1,0] neg_hi:[0,1,0]
	v_pk_add_f32 v[44:45], v[16:17], v[76:77]
	v_pk_add_f32 v[16:17], v[16:17], v[76:77] neg_lo:[0,1] neg_hi:[0,1]
	v_pk_add_f32 v[28:29], v[112:113], v[48:49]
	v_pk_mul_f32 v[76:77], v[16:17], v[34:35] op_sel:[1,0] op_sel_hi:[0,0] neg_lo:[1,1] neg_hi:[0,1]
	v_pk_add_f32 v[48:49], v[112:113], v[48:49] neg_lo:[0,1] neg_hi:[0,1]
	v_pk_fma_f32 v[76:77], v[16:17], v[30:31], v[76:77] op_sel_hi:[1,0,1]
	v_pk_add_f32 v[16:17], v[18:19], v[94:95]
	v_pk_add_f32 v[18:19], v[18:19], v[94:95] neg_lo:[0,1] neg_hi:[0,1]
	s_nop 0
	v_pk_mul_f32 v[94:95], v[18:19], v[10:11] op_sel:[1,0] op_sel_hi:[0,0] neg_lo:[1,1] neg_hi:[0,1]
	s_nop 0
	v_pk_fma_f32 v[18:19], v[18:19], v[10:11], v[94:95] op_sel_hi:[1,0,1]
	v_pk_add_f32 v[94:95], v[20:21], v[96:97]
	v_pk_add_f32 v[20:21], v[20:21], v[96:97] neg_lo:[0,1] neg_hi:[0,1]
	s_nop 0
	v_pk_mul_f32 v[96:97], v[20:21], v[34:35] op_sel_hi:[1,0]
	v_xor_b32_e32 v102, 0x80000000, v21
	v_mov_b32_e32 v103, v20
	v_pk_add_f32 v[20:21], v[22:23], v[98:99]
	v_pk_add_f32 v[22:23], v[22:23], v[98:99] neg_lo:[0,1] neg_hi:[0,1]
	v_pk_fma_f32 v[96:97], v[102:103], v[30:31], v[96:97] op_sel_hi:[1,0,1] neg_lo:[0,1,0] neg_hi:[0,1,0]
	v_xor_b32_e32 v99, 0x80000000, v22
	v_mov_b32_e32 v98, v23
	v_pk_add_f32 v[22:23], v[24:25], v[100:101]
	v_pk_add_f32 v[24:25], v[24:25], v[100:101] neg_lo:[0,1] neg_hi:[0,1]
	s_nop 0
	v_pk_mul_f32 v[100:101], v[24:25], v[34:35] op_sel_hi:[1,0] neg_lo:[0,1] neg_hi:[0,1]
	v_xor_b32_e32 v102, 0x80000000, v25
	v_mov_b32_e32 v103, v24
	v_pk_add_f32 v[24:25], v[26:27], v[32:33]
	v_pk_add_f32 v[26:27], v[26:27], v[32:33] neg_lo:[0,1] neg_hi:[0,1]
	v_pk_fma_f32 v[100:101], v[102:103], v[30:31], v[100:101] op_sel_hi:[1,0,1] neg_lo:[0,1,0] neg_hi:[0,1,0]
	v_pk_mul_f32 v[32:33], v[26:27], v[10:11] op_sel:[1,0] op_sel_hi:[0,0] neg_lo:[1,1] neg_hi:[0,1]
	v_pk_add_f32 v[102:103], v[28:29], v[20:21] neg_lo:[0,1] neg_hi:[0,1]
	v_pk_fma_f32 v[26:27], v[26:27], v[10:11], v[32:33] op_sel_hi:[1,0,1] neg_lo:[0,1,0] neg_hi:[0,1,0]
	v_pk_add_f32 v[32:33], v[40:41], v[36:37]
	v_pk_add_f32 v[36:37], v[40:41], v[36:37] neg_lo:[0,1] neg_hi:[0,1]
	s_nop 0
	v_pk_mul_f32 v[40:41], v[36:37], v[34:35] op_sel:[1,0] op_sel_hi:[0,0] neg_lo:[1,1] neg_hi:[0,1]
	s_nop 0
	v_pk_fma_f32 v[40:41], v[36:37], v[30:31], v[40:41] op_sel_hi:[1,0,1] neg_lo:[0,1,0] neg_hi:[0,1,0]
	v_pk_add_f32 v[36:37], v[28:29], v[20:21]
	v_pk_add_f32 v[20:21], v[44:45], v[22:23]
	v_pk_add_f32 v[22:23], v[44:45], v[22:23] neg_lo:[0,1] neg_hi:[0,1]
	s_nop 0
	v_pk_mul_f32 v[28:29], v[22:23], v[10:11] op_sel:[1,0] op_sel_hi:[0,0] neg_lo:[1,1] neg_hi:[0,1]
	s_nop 0
	v_pk_fma_f32 v[22:23], v[22:23], v[10:11], v[28:29] op_sel_hi:[1,0,1]
	v_pk_add_f32 v[28:29], v[16:17], v[24:25]
	v_pk_add_f32 v[16:17], v[16:17], v[24:25] neg_lo:[0,1] neg_hi:[0,1]
	s_nop 0
	v_xor_b32_e32 v25, 0x80000000, v16
	v_mov_b32_e32 v24, v17
	v_pk_add_f32 v[16:17], v[94:95], v[32:33]
	v_pk_add_f32 v[32:33], v[94:95], v[32:33] neg_lo:[0,1] neg_hi:[0,1]
	s_nop 0
	v_pk_mul_f32 v[44:45], v[32:33], v[10:11] op_sel:[1,0] op_sel_hi:[0,0] neg_lo:[1,1] neg_hi:[0,1]
	s_nop 0
	v_pk_fma_f32 v[32:33], v[32:33], v[10:11], v[44:45] op_sel_hi:[1,0,1] neg_lo:[0,1,0] neg_hi:[0,1,0]
	v_pk_add_f32 v[44:45], v[36:37], v[28:29]
	v_pk_add_f32 v[36:37], v[36:37], v[28:29] neg_lo:[0,1] neg_hi:[0,1]
	v_pk_add_f32 v[28:29], v[20:21], v[16:17]
	v_pk_add_f32 v[16:17], v[20:21], v[16:17] neg_lo:[0,1] neg_hi:[0,1]
	v_pk_add_f32 v[94:95], v[44:45], v[28:29]
	v_xor_b32_e32 v21, 0x80000000, v16
	v_mov_b32_e32 v20, v17
	v_pk_add_f32 v[16:17], v[102:103], v[24:25]
	v_pk_add_f32 v[102:103], v[102:103], v[24:25] neg_lo:[0,1] neg_hi:[0,1]
	v_pk_add_f32 v[24:25], v[22:23], v[32:33]
	v_pk_add_f32 v[22:23], v[22:23], v[32:33] neg_lo:[0,1] neg_hi:[0,1]
	v_pk_add_f32 v[28:29], v[44:45], v[28:29] neg_lo:[0,1] neg_hi:[0,1]
	v_xor_b32_e32 v33, 0x80000000, v22
	v_mov_b32_e32 v32, v23
	v_pk_add_f32 v[22:23], v[48:49], v[98:99]
	v_pk_add_f32 v[98:99], v[48:49], v[98:99] neg_lo:[0,1] neg_hi:[0,1]
	v_pk_add_f32 v[48:49], v[76:77], v[100:101] neg_lo:[0,1] neg_hi:[0,1]
	v_pk_add_f32 v[44:45], v[36:37], v[20:21]
	v_pk_add_f32 v[20:21], v[36:37], v[20:21] neg_lo:[0,1] neg_hi:[0,1]
	v_pk_add_f32 v[104:105], v[16:17], v[24:25]
	v_pk_add_f32 v[24:25], v[16:17], v[24:25] neg_lo:[0,1] neg_hi:[0,1]
	v_pk_add_f32 v[36:37], v[102:103], v[32:33]
	v_pk_add_f32 v[16:17], v[102:103], v[32:33] neg_lo:[0,1] neg_hi:[0,1]
	v_pk_add_f32 v[32:33], v[76:77], v[100:101]
	v_pk_mul_f32 v[76:77], v[10:11], v[48:49] op_sel:[0,1] op_sel_hi:[0,0] neg_lo:[1,1] neg_hi:[1,0]
	v_pk_fma_f32 v[76:77], v[10:11], v[48:49], v[76:77] op_sel_hi:[0,1,1]
	v_pk_add_f32 v[48:49], v[18:19], v[26:27]
	v_pk_add_f32 v[18:19], v[18:19], v[26:27] neg_lo:[0,1] neg_hi:[0,1]
	s_nop 0
	v_xor_b32_e32 v27, 0x80000000, v18
	v_mov_b32_e32 v26, v19
	v_pk_add_f32 v[18:19], v[96:97], v[40:41]
	v_pk_add_f32 v[40:41], v[96:97], v[40:41] neg_lo:[0,1] neg_hi:[0,1]
	s_nop 0
	v_pk_mul_f32 v[96:97], v[10:11], v[40:41] op_sel:[0,1] op_sel_hi:[0,0] neg_lo:[1,1] neg_hi:[1,0]
	v_pk_fma_f32 v[40:41], v[10:11], v[40:41], v[96:97] op_sel_hi:[0,1,1] neg_lo:[1,0,0] neg_hi:[1,0,0]
	v_pk_add_f32 v[96:97], v[22:23], v[48:49]
	v_pk_add_f32 v[22:23], v[22:23], v[48:49] neg_lo:[0,1] neg_hi:[0,1]
	v_pk_add_f32 v[48:49], v[32:33], v[18:19]
	v_pk_add_f32 v[18:19], v[32:33], v[18:19] neg_lo:[0,1] neg_hi:[0,1]
	v_pk_add_f32 v[102:103], v[96:97], v[48:49]
	v_xor_b32_e32 v101, 0x80000000, v18
	v_mov_b32_e32 v100, v19
	v_pk_add_f32 v[32:33], v[96:97], v[48:49] neg_lo:[0,1] neg_hi:[0,1]
	v_pk_add_f32 v[18:19], v[98:99], v[26:27]
	v_pk_add_f32 v[96:97], v[98:99], v[26:27] neg_lo:[0,1] neg_hi:[0,1]
	v_pk_add_f32 v[26:27], v[76:77], v[40:41]
	v_pk_add_f32 v[40:41], v[76:77], v[40:41] neg_lo:[0,1] neg_hi:[0,1]
	v_pk_add_f32 v[98:99], v[18:19], v[26:27]
	v_xor_b32_e32 v77, 0x80000000, v40
	v_mov_b32_e32 v76, v41
	v_pk_add_f32 v[26:27], v[18:19], v[26:27] neg_lo:[0,1] neg_hi:[0,1]
	v_pk_add_f32 v[40:41], v[96:97], v[76:77]
	v_pk_add_f32 v[18:19], v[96:97], v[76:77] neg_lo:[0,1] neg_hi:[0,1]
	v_pk_add_f32 v[76:77], v[38:39], v[92:93]
	v_pk_add_f32 v[92:93], v[38:39], v[92:93] neg_lo:[0,1] neg_hi:[0,1]
	v_pk_add_f32 v[38:39], v[42:43], v[78:79]
	v_pk_add_f32 v[42:43], v[42:43], v[78:79] neg_lo:[0,1] neg_hi:[0,1]
	v_pk_add_f32 v[48:49], v[22:23], v[100:101]
	v_pk_mul_f32 v[78:79], v[34:35], v[42:43] op_sel:[0,1] op_sel_hi:[0,0] neg_lo:[1,1] neg_hi:[1,0]
	v_pk_fma_f32 v[42:43], v[30:31], v[42:43], v[78:79] op_sel_hi:[0,1,1]
	v_pk_add_f32 v[78:79], v[46:47], v[80:81]
	v_pk_add_f32 v[46:47], v[46:47], v[80:81] neg_lo:[0,1] neg_hi:[0,1]
	v_pk_add_f32 v[22:23], v[22:23], v[100:101] neg_lo:[0,1] neg_hi:[0,1]
	v_pk_mul_f32 v[80:81], v[10:11], v[46:47] op_sel:[0,1] op_sel_hi:[0,0] neg_lo:[1,1] neg_hi:[1,0]
	v_pk_fma_f32 v[80:81], v[10:11], v[46:47], v[80:81] op_sel_hi:[0,1,1]
	v_pk_add_f32 v[46:47], v[50:51], v[82:83]
	v_pk_add_f32 v[50:51], v[50:51], v[82:83] neg_lo:[0,1] neg_hi:[0,1]
	s_nop 0
	v_pk_mul_f32 v[82:83], v[30:31], v[50:51] op_sel:[0,1] op_sel_hi:[0,0] neg_lo:[1,1] neg_hi:[1,0]
	v_pk_fma_f32 v[50:51], v[34:35], v[50:51], v[82:83] op_sel_hi:[0,1,1]
	v_pk_add_f32 v[82:83], v[52:53], v[84:85]
	v_pk_add_f32 v[52:53], v[52:53], v[84:85] neg_lo:[0,1] neg_hi:[0,1]
	s_nop 0
	v_xor_b32_e32 v85, 0x80000000, v52
	v_mov_b32_e32 v84, v53
	v_pk_add_f32 v[52:53], v[54:55], v[86:87]
	v_pk_add_f32 v[54:55], v[54:55], v[86:87] neg_lo:[0,1] neg_hi:[0,1]
	s_nop 0
	v_pk_mul_f32 v[86:87], v[30:31], v[54:55] op_sel:[0,1] op_sel_hi:[0,0] neg_lo:[1,1] neg_hi:[1,0]
	v_pk_fma_f32 v[54:55], v[34:35], v[54:55], v[86:87] op_sel_hi:[0,1,1] neg_lo:[1,0,0] neg_hi:[1,0,0]
	v_pk_add_f32 v[86:87], v[56:57], v[88:89]
	v_pk_add_f32 v[56:57], v[56:57], v[88:89] neg_lo:[0,1] neg_hi:[0,1]
	s_nop 0
	v_pk_mul_f32 v[88:89], v[10:11], v[56:57] op_sel:[0,1] op_sel_hi:[0,0] neg_lo:[1,1] neg_hi:[1,0]
	v_pk_fma_f32 v[56:57], v[10:11], v[56:57], v[88:89] op_sel_hi:[0,1,1] neg_lo:[1,0,0] neg_hi:[1,0,0]
	v_pk_add_f32 v[88:89], v[58:59], v[90:91]
	v_pk_add_f32 v[58:59], v[58:59], v[90:91] neg_lo:[0,1] neg_hi:[0,1]
	s_nop 0
	v_pk_mul_f32 v[34:35], v[34:35], v[58:59] op_sel:[0,1] op_sel_hi:[0,0] neg_lo:[1,1] neg_hi:[1,0]
	v_pk_fma_f32 v[34:35], v[30:31], v[58:59], v[34:35] op_sel_hi:[0,1,1] neg_lo:[1,0,0] neg_hi:[1,0,0]
	v_pk_add_f32 v[30:31], v[76:77], v[82:83]
	v_pk_add_f32 v[58:59], v[76:77], v[82:83] neg_lo:[0,1] neg_hi:[0,1]
	v_pk_add_f32 v[76:77], v[52:53], v[38:39]
	v_pk_add_f32 v[38:39], v[38:39], v[52:53] neg_lo:[0,1] neg_hi:[0,1]
	s_nop 0
	v_pk_mul_f32 v[52:53], v[10:11], v[38:39] op_sel:[0,1] op_sel_hi:[0,0] neg_lo:[1,1] neg_hi:[1,0]
	v_pk_fma_f32 v[52:53], v[10:11], v[38:39], v[52:53] op_sel_hi:[0,1,1]
	v_pk_add_f32 v[38:39], v[78:79], v[86:87]
	v_pk_add_f32 v[78:79], v[78:79], v[86:87] neg_lo:[0,1] neg_hi:[0,1]
	s_nop 0
	v_xor_b32_e32 v83, 0x80000000, v78
	v_mov_b32_e32 v82, v79
	v_pk_add_f32 v[78:79], v[46:47], v[88:89]
	v_pk_add_f32 v[46:47], v[46:47], v[88:89] neg_lo:[0,1] neg_hi:[0,1]
	v_pk_add_f32 v[88:89], v[76:77], v[78:79]
	v_pk_mul_f32 v[86:87], v[10:11], v[46:47] op_sel:[0,1] op_sel_hi:[0,0] neg_lo:[1,1] neg_hi:[1,0]
	v_pk_fma_f32 v[46:47], v[10:11], v[46:47], v[86:87] op_sel_hi:[0,1,1] neg_lo:[1,0,0] neg_hi:[1,0,0]
	v_pk_add_f32 v[86:87], v[30:31], v[38:39]
	v_pk_add_f32 v[30:31], v[30:31], v[38:39] neg_lo:[0,1] neg_hi:[0,1]
	v_pk_add_f32 v[38:39], v[76:77], v[78:79] neg_lo:[0,1] neg_hi:[0,1]
	v_pk_add_f32 v[78:79], v[86:87], v[88:89] neg_lo:[0,1] neg_hi:[0,1]
	v_pk_add_f32 v[90:91], v[30:31], v[38:39] op_sel:[0,1] op_sel_hi:[1,0] neg_hi:[0,1]
	v_pk_add_f32 v[38:39], v[30:31], v[38:39] op_sel:[0,1] op_sel_hi:[1,0] neg_lo:[0,1]
	v_pk_add_f32 v[76:77], v[52:53], v[46:47]
	v_pk_add_f32 v[46:47], v[52:53], v[46:47] neg_lo:[0,1] neg_hi:[0,1]
	v_pk_add_f32 v[30:31], v[58:59], v[82:83]
	v_pk_add_f32 v[58:59], v[58:59], v[82:83] neg_lo:[0,1] neg_hi:[0,1]
	v_xor_b32_e32 v53, 0x80000000, v46
	v_mov_b32_e32 v52, v47
	v_pk_add_f32 v[82:83], v[30:31], v[76:77]
	v_pk_add_f32 v[46:47], v[30:31], v[76:77] neg_lo:[0,1] neg_hi:[0,1]
	v_pk_add_f32 v[76:77], v[58:59], v[52:53]
	v_pk_add_f32 v[30:31], v[58:59], v[52:53] neg_lo:[0,1] neg_hi:[0,1]
	v_pk_add_f32 v[52:53], v[92:93], v[84:85]
	v_pk_add_f32 v[58:59], v[92:93], v[84:85] neg_lo:[0,1] neg_hi:[0,1]
	v_pk_add_f32 v[84:85], v[54:55], v[42:43]
	v_pk_add_f32 v[42:43], v[42:43], v[54:55] neg_lo:[0,1] neg_hi:[0,1]
	v_pk_add_f32 v[86:87], v[86:87], v[88:89]
	v_pk_mul_f32 v[54:55], v[10:11], v[42:43] op_sel:[0,1] op_sel_hi:[0,0] neg_lo:[1,1] neg_hi:[1,0]
	v_pk_fma_f32 v[54:55], v[10:11], v[42:43], v[54:55] op_sel_hi:[0,1,1]
	v_pk_add_f32 v[42:43], v[80:81], v[56:57]
	v_pk_add_f32 v[56:57], v[80:81], v[56:57] neg_lo:[0,1] neg_hi:[0,1]
	s_nop 0
	v_xor_b32_e32 v81, 0x80000000, v56
	v_mov_b32_e32 v80, v57
	v_pk_add_f32 v[56:57], v[50:51], v[34:35]
	v_pk_add_f32 v[34:35], v[50:51], v[34:35] neg_lo:[0,1] neg_hi:[0,1]
	s_nop 0
	v_pk_mul_f32 v[50:51], v[10:11], v[34:35] op_sel:[0,1] op_sel_hi:[0,0] neg_lo:[1,1] neg_hi:[1,0]
	v_pk_fma_f32 v[34:35], v[10:11], v[34:35], v[50:51] op_sel_hi:[0,1,1] neg_lo:[1,0,0] neg_hi:[1,0,0]
	v_pk_add_f32 v[50:51], v[52:53], v[42:43]
	v_pk_add_f32 v[42:43], v[52:53], v[42:43] neg_lo:[0,1] neg_hi:[0,1]
	v_pk_add_f32 v[52:53], v[84:85], v[56:57]
	v_pk_add_f32 v[56:57], v[84:85], v[56:57] neg_lo:[0,1] neg_hi:[0,1]
	s_nop 0
	v_xor_b32_e32 v85, 0x80000000, v56
	v_mov_b32_e32 v84, v57
	v_pk_add_f32 v[56:57], v[50:51], v[52:53]
	v_pk_add_f32 v[50:51], v[50:51], v[52:53] neg_lo:[0,1] neg_hi:[0,1]
	v_pk_add_f32 v[52:53], v[42:43], v[84:85]
	v_pk_add_f32 v[42:43], v[42:43], v[84:85] neg_lo:[0,1] neg_hi:[0,1]
	v_pk_add_f32 v[84:85], v[58:59], v[80:81]
	v_pk_add_f32 v[58:59], v[58:59], v[80:81] neg_lo:[0,1] neg_hi:[0,1]
	v_pk_add_f32 v[80:81], v[54:55], v[34:35]
	v_pk_add_f32 v[34:35], v[54:55], v[34:35] neg_lo:[0,1] neg_hi:[0,1]
	v_pk_add_f32 v[92:93], v[84:85], v[80:81]
	v_pk_add_f32 v[80:81], v[84:85], v[80:81] neg_lo:[0,1] neg_hi:[0,1]
	v_pk_add_f32 v[84:85], v[58:59], v[34:35] op_sel:[0,1] op_sel_hi:[1,0] neg_hi:[0,1]
	v_pk_add_f32 v[34:35], v[58:59], v[34:35] op_sel:[0,1] op_sel_hi:[1,0] neg_lo:[0,1]
	v_pk_fma_f32 v[58:59], v[14:15], s[92:93], v[14:15] op_sel:[1,0,0] op_sel_hi:[0,1,1]
	v_pk_mul_f32 v[54:55], v[94:95], s[14:15] op_sel:[1,0] neg_lo:[1,0]
	v_pk_mul_f32 v[88:89], v[58:59], v[86:87] op_sel:[1,1] op_sel_hi:[0,1] neg_lo:[0,1]
	v_pk_fma_f32 v[54:55], v[94:95], s[42:43], v[54:55] op_sel_hi:[0,1,1]
	v_pk_fma_f32 v[86:87], v[58:59], v[86:87], v[88:89] op_sel_hi:[1,0,1]
	ds_write2_b64 v74, v[54:55], v[86:87] offset1:16
	v_pk_mul_f32 v[54:55], v[14:15], v[58:59] op_sel:[1,1] op_sel_hi:[0,1] neg_lo:[0,1]
	v_pk_fma_f32 v[54:55], v[14:15], v[58:59], v[54:55] op_sel_hi:[1,0,1]
	s_nop 0
	v_pk_mul_f32 v[58:59], v[54:55], v[102:103] op_sel:[1,1] op_sel_hi:[0,1] neg_lo:[0,1]
	v_pk_mul_f32 v[74:75], v[14:15], v[54:55] op_sel:[1,1] op_sel_hi:[0,1] neg_lo:[0,1]
	v_pk_fma_f32 v[58:59], v[54:55], v[102:103], v[58:59] op_sel_hi:[1,0,1]
	v_pk_fma_f32 v[54:55], v[14:15], v[54:55], v[74:75] op_sel_hi:[1,0,1]
	s_nop 0
	v_pk_mul_f32 v[74:75], v[54:55], v[56:57] op_sel:[1,1] op_sel_hi:[0,1] neg_lo:[0,1]
	v_pk_fma_f32 v[56:57], v[54:55], v[56:57], v[74:75] op_sel_hi:[1,0,1]
	ds_write2_b64 v73, v[58:59], v[56:57] offset0:32 offset1:48
	v_pk_mul_f32 v[56:57], v[14:15], v[54:55] op_sel:[1,1] op_sel_hi:[0,1] neg_lo:[0,1]
	v_pk_fma_f32 v[54:55], v[14:15], v[54:55], v[56:57] op_sel_hi:[1,0,1]
	s_nop 0
	v_pk_mul_f32 v[56:57], v[54:55], v[104:105] op_sel:[1,1] op_sel_hi:[0,1] neg_lo:[0,1]
	v_pk_mul_f32 v[58:59], v[14:15], v[54:55] op_sel:[1,1] op_sel_hi:[0,1] neg_lo:[0,1]
	v_pk_fma_f32 v[56:57], v[54:55], v[104:105], v[56:57] op_sel_hi:[1,0,1]
	v_pk_fma_f32 v[54:55], v[14:15], v[54:55], v[58:59] op_sel_hi:[1,0,1]
	s_nop 0
	v_pk_mul_f32 v[58:59], v[54:55], v[82:83] op_sel:[1,1] op_sel_hi:[0,1] neg_lo:[0,1]
	v_pk_fma_f32 v[58:59], v[54:55], v[82:83], v[58:59] op_sel_hi:[1,0,1]
	ds_write2_b64 v72, v[56:57], v[58:59] offset0:64 offset1:80
	v_pk_mul_f32 v[56:57], v[14:15], v[54:55] op_sel:[1,1] op_sel_hi:[0,1] neg_lo:[0,1]
	v_pk_fma_f32 v[54:55], v[14:15], v[54:55], v[56:57] op_sel_hi:[1,0,1]
	s_nop 0
	v_pk_mul_f32 v[56:57], v[54:55], v[98:99] op_sel:[1,1] op_sel_hi:[0,1] neg_lo:[0,1]
	v_pk_mul_f32 v[58:59], v[14:15], v[54:55] op_sel:[1,1] op_sel_hi:[0,1] neg_lo:[0,1]
	v_pk_fma_f32 v[56:57], v[54:55], v[98:99], v[56:57] op_sel_hi:[1,0,1]
	v_pk_fma_f32 v[54:55], v[14:15], v[54:55], v[58:59] op_sel_hi:[1,0,1]
	s_nop 0
	v_pk_mul_f32 v[58:59], v[54:55], v[92:93] op_sel:[1,1] op_sel_hi:[0,1] neg_lo:[0,1]
	v_pk_fma_f32 v[58:59], v[54:55], v[92:93], v[58:59] op_sel_hi:[1,0,1]
	ds_write2_b64 v71, v[56:57], v[58:59] offset0:96 offset1:112
	v_pk_mul_f32 v[56:57], v[14:15], v[54:55] op_sel:[1,1] op_sel_hi:[0,1] neg_lo:[0,1]
	v_pk_fma_f32 v[54:55], v[14:15], v[54:55], v[56:57] op_sel_hi:[1,0,1]
	s_nop 0
	v_pk_mul_f32 v[56:57], v[54:55], v[44:45] op_sel:[1,1] op_sel_hi:[0,1] neg_lo:[0,1]
	v_pk_fma_f32 v[44:45], v[54:55], v[44:45], v[56:57] op_sel_hi:[1,0,1]
	v_pk_mul_f32 v[56:57], v[14:15], v[54:55] op_sel:[1,1] op_sel_hi:[0,1] neg_lo:[0,1]
	v_pk_fma_f32 v[54:55], v[14:15], v[54:55], v[56:57] op_sel_hi:[1,0,1]
	s_nop 0
	v_pk_mul_f32 v[56:57], v[54:55], v[90:91] op_sel:[1,1] op_sel_hi:[0,1] neg_lo:[0,1]
	v_pk_fma_f32 v[56:57], v[54:55], v[90:91], v[56:57] op_sel_hi:[1,0,1]
	ds_write2_b64 v70, v[44:45], v[56:57] offset0:128 offset1:144
	v_pk_mul_f32 v[44:45], v[14:15], v[54:55] op_sel:[1,1] op_sel_hi:[0,1] neg_lo:[0,1]
	v_pk_fma_f32 v[44:45], v[14:15], v[54:55], v[44:45] op_sel_hi:[1,0,1]
	s_nop 0
	v_pk_mul_f32 v[54:55], v[44:45], v[48:49] op_sel:[1,1] op_sel_hi:[0,1] neg_lo:[0,1]
	v_pk_fma_f32 v[48:49], v[44:45], v[48:49], v[54:55] op_sel_hi:[1,0,1]
	v_pk_mul_f32 v[54:55], v[14:15], v[44:45] op_sel:[1,1] op_sel_hi:[0,1] neg_lo:[0,1]
	v_pk_fma_f32 v[44:45], v[14:15], v[44:45], v[54:55] op_sel_hi:[1,0,1]
	s_nop 0
	v_pk_mul_f32 v[54:55], v[44:45], v[52:53] op_sel:[1,1] op_sel_hi:[0,1] neg_lo:[0,1]
	v_pk_fma_f32 v[52:53], v[44:45], v[52:53], v[54:55] op_sel_hi:[1,0,1]
	ds_write2_b64 v69, v[48:49], v[52:53] offset0:160 offset1:176
	v_pk_mul_f32 v[48:49], v[14:15], v[44:45] op_sel:[1,1] op_sel_hi:[0,1] neg_lo:[0,1]
	v_pk_fma_f32 v[44:45], v[14:15], v[44:45], v[48:49] op_sel_hi:[1,0,1]
	s_nop 0
	v_pk_mul_f32 v[48:49], v[36:37], v[44:45] op_sel:[1,1] op_sel_hi:[1,0] neg_lo:[1,0]
	s_nop 0
	v_pk_fma_f32 v[36:37], v[36:37], v[44:45], v[48:49] op_sel_hi:[0,1,1]
	v_pk_mul_f32 v[48:49], v[14:15], v[44:45] op_sel:[1,1] op_sel_hi:[0,1] neg_lo:[0,1]
	v_pk_fma_f32 v[44:45], v[14:15], v[44:45], v[48:49] op_sel_hi:[1,0,1]
	s_nop 0
	v_pk_mul_f32 v[48:49], v[44:45], v[76:77] op_sel:[1,1] op_sel_hi:[0,1] neg_lo:[0,1]
	v_pk_fma_f32 v[48:49], v[44:45], v[76:77], v[48:49] op_sel_hi:[1,0,1]
	ds_write2_b64 v68, v[36:37], v[48:49] offset0:192 offset1:208
	v_pk_mul_f32 v[36:37], v[14:15], v[44:45] op_sel:[1,1] op_sel_hi:[0,1] neg_lo:[0,1]
	v_pk_fma_f32 v[36:37], v[14:15], v[44:45], v[36:37] op_sel_hi:[1,0,1]
	s_nop 0
	v_pk_mul_f32 v[44:45], v[40:41], v[36:37] op_sel:[1,1] op_sel_hi:[1,0] neg_lo:[1,0]
	s_nop 0
	v_pk_fma_f32 v[40:41], v[40:41], v[36:37], v[44:45] op_sel_hi:[0,1,1]
	v_pk_mul_f32 v[44:45], v[14:15], v[36:37] op_sel:[1,1] op_sel_hi:[0,1] neg_lo:[0,1]
	v_pk_fma_f32 v[36:37], v[14:15], v[36:37], v[44:45] op_sel_hi:[1,0,1]
	s_nop 0
	v_pk_mul_f32 v[44:45], v[36:37], v[84:85] op_sel:[1,1] op_sel_hi:[0,1] neg_lo:[0,1]
	v_pk_fma_f32 v[44:45], v[36:37], v[84:85], v[44:45] op_sel_hi:[1,0,1]
	ds_write2_b64 v67, v[40:41], v[44:45] offset0:224 offset1:240
	v_pk_mul_f32 v[40:41], v[14:15], v[36:37] op_sel:[1,1] op_sel_hi:[0,1] neg_lo:[0,1]
	v_pk_fma_f32 v[36:37], v[14:15], v[36:37], v[40:41] op_sel_hi:[1,0,1]
	s_nop 0
	v_pk_mul_f32 v[40:41], v[28:29], v[36:37] op_sel:[1,1] op_sel_hi:[1,0] neg_lo:[1,0]
	s_nop 0
	v_pk_fma_f32 v[28:29], v[28:29], v[36:37], v[40:41] op_sel_hi:[0,1,1]
	v_pk_mul_f32 v[40:41], v[14:15], v[36:37] op_sel:[1,1] op_sel_hi:[0,1] neg_lo:[0,1]
	v_pk_fma_f32 v[36:37], v[14:15], v[36:37], v[40:41] op_sel_hi:[1,0,1]
	s_nop 0
	v_pk_mul_f32 v[40:41], v[78:79], v[36:37] op_sel:[1,1] op_sel_hi:[1,0] neg_lo:[1,0]
	s_nop 0
	v_pk_fma_f32 v[40:41], v[78:79], v[36:37], v[40:41] op_sel_hi:[0,1,1]
	ds_write2_b64 v66, v[28:29], v[40:41] offset1:16
	v_pk_mul_f32 v[28:29], v[14:15], v[36:37] op_sel:[1,1] op_sel_hi:[0,1] neg_lo:[0,1]
	v_pk_fma_f32 v[28:29], v[14:15], v[36:37], v[28:29] op_sel_hi:[1,0,1]
	s_nop 0
	v_pk_mul_f32 v[36:37], v[32:33], v[28:29] op_sel:[1,1] op_sel_hi:[1,0] neg_lo:[1,0]
	s_nop 0
	v_pk_fma_f32 v[32:33], v[32:33], v[28:29], v[36:37] op_sel_hi:[0,1,1]
	v_pk_mul_f32 v[36:37], v[14:15], v[28:29] op_sel:[1,1] op_sel_hi:[0,1] neg_lo:[0,1]
	v_pk_fma_f32 v[28:29], v[14:15], v[28:29], v[36:37] op_sel_hi:[1,0,1]
	s_nop 0
	v_pk_mul_f32 v[36:37], v[50:51], v[28:29] op_sel:[1,1] op_sel_hi:[1,0] neg_lo:[1,0]
	s_nop 0
	v_pk_fma_f32 v[36:37], v[50:51], v[28:29], v[36:37] op_sel_hi:[0,1,1]
	ds_write2_b64 v65, v[32:33], v[36:37] offset0:32 offset1:48
	v_pk_mul_f32 v[32:33], v[14:15], v[28:29] op_sel:[1,1] op_sel_hi:[0,1] neg_lo:[0,1]
	v_pk_fma_f32 v[28:29], v[14:15], v[28:29], v[32:33] op_sel_hi:[1,0,1]
	s_nop 0
	v_pk_mul_f32 v[32:33], v[24:25], v[28:29] op_sel:[1,1] op_sel_hi:[1,0] neg_lo:[1,0]
	s_nop 0
	v_pk_fma_f32 v[24:25], v[24:25], v[28:29], v[32:33] op_sel_hi:[0,1,1]
	v_pk_mul_f32 v[32:33], v[14:15], v[28:29] op_sel:[1,1] op_sel_hi:[0,1] neg_lo:[0,1]
	v_pk_fma_f32 v[28:29], v[14:15], v[28:29], v[32:33] op_sel_hi:[1,0,1]
	s_nop 0
	v_pk_mul_f32 v[32:33], v[46:47], v[28:29] op_sel:[1,1] op_sel_hi:[1,0] neg_lo:[1,0]
	s_nop 0
	v_pk_fma_f32 v[32:33], v[46:47], v[28:29], v[32:33] op_sel_hi:[0,1,1]
	ds_write2_b64 v64, v[24:25], v[32:33] offset0:64 offset1:80
	v_pk_mul_f32 v[24:25], v[14:15], v[28:29] op_sel:[1,1] op_sel_hi:[0,1] neg_lo:[0,1]
	v_pk_fma_f32 v[24:25], v[14:15], v[28:29], v[24:25] op_sel_hi:[1,0,1]
	s_nop 0
	v_pk_mul_f32 v[28:29], v[26:27], v[24:25] op_sel:[1,1] op_sel_hi:[1,0] neg_lo:[1,0]
	s_nop 0
	v_pk_fma_f32 v[26:27], v[26:27], v[24:25], v[28:29] op_sel_hi:[0,1,1]
	v_pk_mul_f32 v[28:29], v[14:15], v[24:25] op_sel:[1,1] op_sel_hi:[0,1] neg_lo:[0,1]
	v_pk_fma_f32 v[24:25], v[14:15], v[24:25], v[28:29] op_sel_hi:[1,0,1]
	s_nop 0
	v_pk_mul_f32 v[28:29], v[80:81], v[24:25] op_sel:[1,1] op_sel_hi:[1,0] neg_lo:[1,0]
	s_nop 0
	v_pk_fma_f32 v[28:29], v[80:81], v[24:25], v[28:29] op_sel_hi:[0,1,1]
	ds_write2_b64 v63, v[26:27], v[28:29] offset0:96 offset1:112
	v_pk_mul_f32 v[26:27], v[14:15], v[24:25] op_sel:[1,1] op_sel_hi:[0,1] neg_lo:[0,1]
	v_pk_fma_f32 v[24:25], v[14:15], v[24:25], v[26:27] op_sel_hi:[1,0,1]
	s_nop 0
	v_pk_mul_f32 v[26:27], v[20:21], v[24:25] op_sel:[1,1] op_sel_hi:[1,0] neg_lo:[1,0]
	s_nop 0
	v_pk_fma_f32 v[20:21], v[20:21], v[24:25], v[26:27] op_sel_hi:[0,1,1]
	v_pk_mul_f32 v[26:27], v[14:15], v[24:25] op_sel:[1,1] op_sel_hi:[0,1] neg_lo:[0,1]
	v_pk_fma_f32 v[24:25], v[14:15], v[24:25], v[26:27] op_sel_hi:[1,0,1]
	s_nop 0
	v_pk_mul_f32 v[26:27], v[38:39], v[24:25] op_sel:[1,1] op_sel_hi:[1,0] neg_lo:[1,0]
	s_nop 0
	v_pk_fma_f32 v[26:27], v[38:39], v[24:25], v[26:27] op_sel_hi:[0,1,1]
	ds_write2_b64 v62, v[20:21], v[26:27] offset0:128 offset1:144
	v_pk_mul_f32 v[20:21], v[14:15], v[24:25] op_sel:[1,1] op_sel_hi:[0,1] neg_lo:[0,1]
	v_pk_fma_f32 v[20:21], v[14:15], v[24:25], v[20:21] op_sel_hi:[1,0,1]
	s_nop 0
	v_pk_mul_f32 v[24:25], v[22:23], v[20:21] op_sel:[1,1] op_sel_hi:[1,0] neg_lo:[1,0]
	s_nop 0
	v_pk_fma_f32 v[22:23], v[22:23], v[20:21], v[24:25] op_sel_hi:[0,1,1]
	v_pk_mul_f32 v[24:25], v[14:15], v[20:21] op_sel:[1,1] op_sel_hi:[0,1] neg_lo:[0,1]
	v_pk_fma_f32 v[20:21], v[14:15], v[20:21], v[24:25] op_sel_hi:[1,0,1]
	s_nop 0
	v_pk_mul_f32 v[24:25], v[42:43], v[20:21] op_sel:[1,1] op_sel_hi:[1,0] neg_lo:[1,0]
	s_nop 0
	v_pk_fma_f32 v[24:25], v[42:43], v[20:21], v[24:25] op_sel_hi:[0,1,1]
	ds_write2_b64 v61, v[22:23], v[24:25] offset0:160 offset1:176
	v_pk_mul_f32 v[22:23], v[14:15], v[20:21] op_sel:[1,1] op_sel_hi:[0,1] neg_lo:[0,1]
	v_pk_fma_f32 v[20:21], v[14:15], v[20:21], v[22:23] op_sel_hi:[1,0,1]
	s_nop 0
	v_pk_mul_f32 v[22:23], v[16:17], v[20:21] op_sel:[1,1] op_sel_hi:[1,0] neg_lo:[1,0]
	s_nop 0
	v_pk_fma_f32 v[16:17], v[16:17], v[20:21], v[22:23] op_sel_hi:[0,1,1]
	v_pk_mul_f32 v[22:23], v[14:15], v[20:21] op_sel:[1,1] op_sel_hi:[0,1] neg_lo:[0,1]
	v_pk_fma_f32 v[20:21], v[14:15], v[20:21], v[22:23] op_sel_hi:[1,0,1]
	s_nop 0
	v_pk_mul_f32 v[22:23], v[30:31], v[20:21] op_sel:[1,1] op_sel_hi:[1,0] neg_lo:[1,0]
	s_nop 0
	v_pk_fma_f32 v[22:23], v[30:31], v[20:21], v[22:23] op_sel_hi:[0,1,1]
	ds_write2_b64 v60, v[16:17], v[22:23] offset0:192 offset1:208
	v_pk_mul_f32 v[16:17], v[14:15], v[20:21] op_sel:[1,1] op_sel_hi:[0,1] neg_lo:[0,1]
	v_pk_fma_f32 v[16:17], v[14:15], v[20:21], v[16:17] op_sel_hi:[1,0,1]
	s_nop 0
	v_pk_mul_f32 v[20:21], v[18:19], v[16:17] op_sel:[1,1] op_sel_hi:[1,0] neg_lo:[1,0]
	s_nop 0
	v_pk_fma_f32 v[18:19], v[18:19], v[16:17], v[20:21] op_sel_hi:[0,1,1]
	v_pk_mul_f32 v[20:21], v[14:15], v[16:17] op_sel:[1,1] op_sel_hi:[0,1] neg_lo:[0,1]
	v_pk_fma_f32 v[14:15], v[14:15], v[16:17], v[20:21] op_sel_hi:[1,0,1]
	s_nop 0
	v_pk_mul_f32 v[16:17], v[34:35], v[14:15] op_sel:[1,1] op_sel_hi:[1,0] neg_lo:[1,0]
	s_nop 0
	v_pk_fma_f32 v[14:15], v[34:35], v[14:15], v[16:17] op_sel_hi:[0,1,1]
	ds_write2_b64 v13, v[18:19], v[14:15] offset0:224 offset1:240
	v_mov_b32_e32 v14, v1
	v_mov_b32_e32 v10, v178
	v_mov_b32_e32 v13, v177
	s_waitcnt lgkmcnt(0)
	s_barrier
	v_mov_b32_e32 v48, v168
	v_xor_b32_e32 v16, 1, v13
	v_lshlrev_b32_e32 v10, 3, v10
	v_lshlrev_b32_e32 v16, 3, v16
	v_add3_u32 v18, 0, v16, v10
	v_xor_b32_e32 v16, 2, v13
	v_lshlrev_b32_e32 v16, 3, v16
	v_xor_b32_e32 v24, 5, v13
	v_add3_u32 v20, 0, v16, v10
	v_xor_b32_e32 v16, 3, v13
	v_lshlrev_b32_e32 v24, 3, v24
	v_lshlrev_b32_e32 v15, 3, v13
	v_lshlrev_b32_e32 v16, 3, v16
	v_add3_u32 v26, 0, v24, v10
	v_xor_b32_e32 v24, 6, v13
	v_add3_u32 v15, 0, v15, v10
	v_add3_u32 v22, 0, v16, v10
	v_lshlrev_b32_e32 v24, 3, v24
	v_xor_b32_e32 v32, 9, v13
	ds_read_b64 v[16:17], v15
	ds_read_b64 v[18:19], v18
	ds_read_b64 v[20:21], v20
	ds_read_b64 v[22:23], v22
	v_xor_b32_e32 v15, 4, v13
	v_add3_u32 v28, 0, v24, v10
	v_xor_b32_e32 v24, 7, v13
	v_lshlrev_b32_e32 v32, 3, v32
	v_lshlrev_b32_e32 v15, 3, v15
	v_lshlrev_b32_e32 v24, 3, v24
	v_add3_u32 v34, 0, v32, v10
	v_xor_b32_e32 v32, 10, v13
	v_add3_u32 v15, 0, v15, v10
	v_add3_u32 v30, 0, v24, v10
	v_lshlrev_b32_e32 v32, 3, v32
	ds_read_b64 v[24:25], v15
	ds_read_b64 v[26:27], v26
	ds_read_b64 v[28:29], v28
	ds_read_b64 v[30:31], v30
	v_xor_b32_e32 v15, 8, v13
	v_add3_u32 v36, 0, v32, v10
	v_xor_b32_e32 v32, 11, v13
	v_lshlrev_b32_e32 v15, 3, v15
	v_lshlrev_b32_e32 v32, 3, v32
	v_xor_b32_e32 v40, 13, v13
	v_add3_u32 v15, 0, v15, v10
	v_add3_u32 v38, 0, v32, v10
	v_lshlrev_b32_e32 v40, 3, v40
	ds_read_b64 v[32:33], v15
	ds_read_b64 v[34:35], v34
	ds_read_b64 v[36:37], v36
	ds_read_b64 v[38:39], v38
	v_xor_b32_e32 v15, 12, v13
	v_add3_u32 v42, 0, v40, v10
	v_xor_b32_e32 v40, 14, v13
	v_xor_b32_e32 v13, 15, v13
	v_lshlrev_b32_e32 v15, 3, v15
	v_lshlrev_b32_e32 v40, 3, v40
	v_lshlrev_b32_e32 v13, 3, v13
	v_add3_u32 v15, 0, v15, v10
	v_add3_u32 v44, 0, v40, v10
	v_add3_u32 v10, 0, v13, v10
	ds_read_b64 v[40:41], v15
	ds_read_b64 v[42:43], v42
	ds_read_b64 v[44:45], v44
	ds_read_b64 v[46:47], v10
	v_mov_b32_e32 v10, v164
	v_mov_b32_e32 v13, v167
	v_mov_b32_e32 v10, v165
	s_waitcnt lgkmcnt(7)
	v_pk_add_f32 v[52:53], v[16:17], v[32:33]
	v_mov_b32_e32 v10, v166
	v_pk_add_f32 v[16:17], v[16:17], v[32:33] neg_lo:[0,1] neg_hi:[0,1]
	s_waitcnt lgkmcnt(6)
	v_pk_add_f32 v[32:33], v[18:19], v[34:35]
	v_pk_add_f32 v[18:19], v[18:19], v[34:35] neg_lo:[0,1] neg_hi:[0,1]
	v_mov_b32_e32 v13, v169
	v_mov_b32_e32 v50, v170
	v_ashrrev_i32_e32 v15, 31, v14
	v_pk_mul_f32 v[34:35], v[18:19], v[50:51] op_sel:[1,0] op_sel_hi:[0,0] neg_lo:[1,1] neg_hi:[0,1]
	v_mov_b32_e32 v13, v171
	v_pk_fma_f32 v[18:19], v[18:19], v[10:11], v[34:35] op_sel_hi:[1,0,1]
	s_waitcnt lgkmcnt(5)
	v_pk_add_f32 v[34:35], v[20:21], v[36:37]
	v_pk_add_f32 v[20:21], v[20:21], v[36:37] neg_lo:[0,1] neg_hi:[0,1]
	s_mov_b32 s39, 0x8000
	v_pk_mul_f32 v[36:37], v[20:21], v[48:49] op_sel:[1,0] op_sel_hi:[0,0] neg_lo:[1,1] neg_hi:[0,1]
	v_mov_b32_e32 v13, v172
	v_pk_fma_f32 v[20:21], v[20:21], v[48:49], v[36:37] op_sel_hi:[1,0,1]
	s_waitcnt lgkmcnt(4)
	v_pk_add_f32 v[36:37], v[22:23], v[38:39]
	v_pk_add_f32 v[22:23], v[22:23], v[38:39] neg_lo:[0,1] neg_hi:[0,1]
	s_nop 0
	v_pk_mul_f32 v[38:39], v[22:23], v[50:51] op_sel_hi:[1,0]
	s_nop 0
	v_pk_fma_f32 v[22:23], v[22:23], v[10:11], v[38:39] op_sel:[1,0,0] op_sel_hi:[0,0,1] neg_lo:[1,1,0] neg_hi:[0,1,0]
	s_waitcnt lgkmcnt(3)
	v_pk_add_f32 v[38:39], v[24:25], v[40:41]
	v_pk_add_f32 v[24:25], v[24:25], v[40:41] neg_lo:[0,1] neg_hi:[0,1]
	v_mov_b32_e32 v13, v177
	v_xor_b32_e32 v41, 0x80000000, v24
	v_mov_b32_e32 v40, v25
	s_waitcnt lgkmcnt(2)
	v_pk_add_f32 v[24:25], v[26:27], v[42:43]
	v_pk_add_f32 v[26:27], v[26:27], v[42:43] neg_lo:[0,1] neg_hi:[0,1]
	s_nop 0
	v_pk_mul_f32 v[42:43], v[26:27], v[50:51] op_sel_hi:[1,0] neg_lo:[0,1] neg_hi:[0,1]
	s_nop 0
	v_pk_fma_f32 v[26:27], v[26:27], v[10:11], v[42:43] op_sel:[1,0,0] op_sel_hi:[0,0,1] neg_lo:[1,1,0] neg_hi:[0,1,0]
	s_waitcnt lgkmcnt(1)
	v_pk_add_f32 v[42:43], v[28:29], v[44:45]
	v_pk_add_f32 v[28:29], v[28:29], v[44:45] neg_lo:[0,1] neg_hi:[0,1]
	s_nop 0
	v_pk_mul_f32 v[44:45], v[28:29], v[48:49] op_sel:[1,0] op_sel_hi:[0,0] neg_lo:[1,1] neg_hi:[0,1]
	s_nop 0
	v_pk_fma_f32 v[28:29], v[28:29], v[48:49], v[44:45] op_sel_hi:[1,0,1] neg_lo:[0,1,0] neg_hi:[0,1,0]
	s_waitcnt lgkmcnt(0)
	v_pk_add_f32 v[44:45], v[30:31], v[46:47]
	v_pk_add_f32 v[30:31], v[30:31], v[46:47] neg_lo:[0,1] neg_hi:[0,1]
	s_nop 0
	v_pk_mul_f32 v[46:47], v[30:31], v[50:51] op_sel:[1,0] op_sel_hi:[0,0] neg_lo:[1,1] neg_hi:[0,1]
	v_pk_add_f32 v[50:51], v[32:33], v[24:25]
	v_pk_add_f32 v[24:25], v[32:33], v[24:25] neg_lo:[0,1] neg_hi:[0,1]
	v_pk_fma_f32 v[30:31], v[30:31], v[10:11], v[46:47] op_sel_hi:[1,0,1] neg_lo:[0,1,0] neg_hi:[0,1,0]
	v_pk_mul_f32 v[32:33], v[24:25], v[48:49] op_sel:[1,0] op_sel_hi:[0,0] neg_lo:[1,1] neg_hi:[0,1]
	v_pk_add_f32 v[46:47], v[52:53], v[38:39]
	v_pk_fma_f32 v[24:25], v[24:25], v[48:49], v[32:33] op_sel_hi:[1,0,1]
	v_pk_add_f32 v[32:33], v[34:35], v[42:43]
	v_pk_add_f32 v[34:35], v[34:35], v[42:43] neg_lo:[0,1] neg_hi:[0,1]
	v_pk_add_f32 v[38:39], v[52:53], v[38:39] neg_lo:[0,1] neg_hi:[0,1]
	v_xor_b32_e32 v43, 0x80000000, v34
	v_mov_b32_e32 v42, v35
	v_pk_add_f32 v[34:35], v[36:37], v[44:45]
	v_pk_add_f32 v[36:37], v[36:37], v[44:45] neg_lo:[0,1] neg_hi:[0,1]
	v_mov_b32_e32 v10, v179
	v_pk_mul_f32 v[44:45], v[36:37], v[48:49] op_sel:[1,0] op_sel_hi:[0,0] neg_lo:[1,1] neg_hi:[0,1]
	s_nop 0
	v_pk_fma_f32 v[36:37], v[36:37], v[48:49], v[44:45] op_sel_hi:[1,0,1] neg_lo:[0,1,0] neg_hi:[0,1,0]
	v_pk_add_f32 v[44:45], v[46:47], v[32:33]
	v_pk_add_f32 v[32:33], v[46:47], v[32:33] neg_lo:[0,1] neg_hi:[0,1]
	v_pk_add_f32 v[46:47], v[50:51], v[34:35]
	v_pk_add_f32 v[34:35], v[50:51], v[34:35] neg_lo:[0,1] neg_hi:[0,1]
	s_nop 0
	v_xor_b32_e32 v51, 0x80000000, v34
	v_mov_b32_e32 v50, v35
	v_pk_add_f32 v[34:35], v[44:45], v[46:47]
	v_pk_add_f32 v[44:45], v[44:45], v[46:47] neg_lo:[0,1] neg_hi:[0,1]
	v_pk_add_f32 v[46:47], v[32:33], v[50:51]
	v_pk_add_f32 v[32:33], v[32:33], v[50:51] neg_lo:[0,1] neg_hi:[0,1]
	v_pk_add_f32 v[50:51], v[38:39], v[42:43]
	v_pk_add_f32 v[38:39], v[38:39], v[42:43] neg_lo:[0,1] neg_hi:[0,1]
	v_pk_add_f32 v[42:43], v[24:25], v[36:37]
	v_pk_add_f32 v[24:25], v[24:25], v[36:37] neg_lo:[0,1] neg_hi:[0,1]
	s_nop 0
	v_xor_b32_e32 v37, 0x80000000, v24
	v_mov_b32_e32 v36, v25
	v_pk_add_f32 v[24:25], v[50:51], v[42:43]
	v_pk_add_f32 v[42:43], v[50:51], v[42:43] neg_lo:[0,1] neg_hi:[0,1]
	v_pk_add_f32 v[50:51], v[38:39], v[36:37]
	v_pk_add_f32 v[36:37], v[38:39], v[36:37] neg_lo:[0,1] neg_hi:[0,1]
	v_pk_add_f32 v[38:39], v[16:17], v[40:41]
	v_pk_add_f32 v[16:17], v[16:17], v[40:41] neg_lo:[0,1] neg_hi:[0,1]
	v_pk_add_f32 v[40:41], v[18:19], v[26:27]
	v_pk_add_f32 v[18:19], v[18:19], v[26:27] neg_lo:[0,1] neg_hi:[0,1]
	s_nop 0
	v_pk_mul_f32 v[26:27], v[48:49], v[18:19] op_sel:[0,1] op_sel_hi:[0,0] neg_lo:[1,1] neg_hi:[1,0]
	v_pk_fma_f32 v[18:19], v[48:49], v[18:19], v[26:27] op_sel_hi:[0,1,1]
	v_pk_add_f32 v[26:27], v[20:21], v[28:29]
	v_pk_add_f32 v[20:21], v[20:21], v[28:29] neg_lo:[0,1] neg_hi:[0,1]
	s_nop 0
	v_xor_b32_e32 v29, 0x80000000, v20
	v_mov_b32_e32 v28, v21
	v_pk_add_f32 v[20:21], v[22:23], v[30:31]
	v_pk_add_f32 v[22:23], v[22:23], v[30:31] neg_lo:[0,1] neg_hi:[0,1]
	s_nop 0
	v_pk_mul_f32 v[30:31], v[48:49], v[22:23] op_sel:[0,1] op_sel_hi:[0,0] neg_lo:[1,1] neg_hi:[1,0]
	v_pk_fma_f32 v[22:23], v[48:49], v[22:23], v[30:31] op_sel_hi:[0,1,1] neg_lo:[1,0,0] neg_hi:[1,0,0]
	v_pk_add_f32 v[30:31], v[38:39], v[26:27]
	v_pk_add_f32 v[26:27], v[38:39], v[26:27] neg_lo:[0,1] neg_hi:[0,1]
	v_pk_add_f32 v[38:39], v[40:41], v[20:21]
	v_pk_add_f32 v[20:21], v[40:41], v[20:21] neg_lo:[0,1] neg_hi:[0,1]
	v_mov_b32_e32 v48, v168
	v_xor_b32_e32 v41, 0x80000000, v20
	v_mov_b32_e32 v40, v21
	v_pk_add_f32 v[20:21], v[30:31], v[38:39]
	v_pk_add_f32 v[30:31], v[30:31], v[38:39] neg_lo:[0,1] neg_hi:[0,1]
	v_pk_add_f32 v[38:39], v[26:27], v[40:41]
	v_pk_add_f32 v[26:27], v[26:27], v[40:41] neg_lo:[0,1] neg_hi:[0,1]
	v_pk_add_f32 v[40:41], v[16:17], v[28:29]
	v_pk_add_f32 v[16:17], v[16:17], v[28:29] neg_lo:[0,1] neg_hi:[0,1]
	v_pk_add_f32 v[28:29], v[18:19], v[22:23]
	v_pk_add_f32 v[18:19], v[18:19], v[22:23] neg_lo:[0,1] neg_hi:[0,1]
	s_nop 0
	v_xor_b32_e32 v23, 0x80000000, v18
	v_mov_b32_e32 v22, v19
	v_pk_add_f32 v[18:19], v[40:41], v[28:29]
	v_pk_add_f32 v[28:29], v[40:41], v[28:29] neg_lo:[0,1] neg_hi:[0,1]
	v_pk_add_f32 v[40:41], v[16:17], v[22:23]
	v_pk_add_f32 v[16:17], v[16:17], v[22:23] neg_lo:[0,1] neg_hi:[0,1]
	v_lshl_add_u64 v[22:23], v[14:15], 3, s[48:49]
	global_store_dwordx2 v[22:23], v[34:35], off
	v_add_u32_e32 v22, 0x200, v14
	v_ashrrev_i32_e32 v23, 31, v22
	v_lshl_add_u64 v[22:23], v[22:23], 3, s[48:49]
	global_store_dwordx2 v[22:23], v[20:21], off
	v_add_u32_e32 v20, 0x400, v14
	v_ashrrev_i32_e32 v21, 31, v20
	v_lshl_add_u64 v[20:21], v[20:21], 3, s[48:49]
	global_store_dwordx2 v[20:21], v[24:25], off
	v_add_u32_e32 v20, 0x600, v14
	v_ashrrev_i32_e32 v21, 31, v20
	v_lshl_add_u64 v[20:21], v[20:21], 3, s[48:49]
	global_store_dwordx2 v[20:21], v[18:19], off
	v_add_u32_e32 v18, 0x800, v14
	v_ashrrev_i32_e32 v19, 31, v18
	v_lshl_add_u64 v[18:19], v[18:19], 3, s[48:49]
	global_store_dwordx2 v[18:19], v[46:47], off
	v_add_u32_e32 v18, 0xa00, v14
	v_ashrrev_i32_e32 v19, 31, v18
	v_lshl_add_u64 v[18:19], v[18:19], 3, s[48:49]
	global_store_dwordx2 v[18:19], v[38:39], off
	v_add_u32_e32 v18, 0xc00, v14
	v_ashrrev_i32_e32 v19, 31, v18
	v_lshl_add_u64 v[18:19], v[18:19], 3, s[48:49]
	global_store_dwordx2 v[18:19], v[50:51], off
	v_add_u32_e32 v18, 0xe00, v14
	v_ashrrev_i32_e32 v19, 31, v18
	v_lshl_add_u64 v[18:19], v[18:19], 3, s[48:49]
	global_store_dwordx2 v[18:19], v[40:41], off
	v_add_u32_e32 v18, 0x1000, v14
	v_ashrrev_i32_e32 v19, 31, v18
	v_lshl_add_u64 v[18:19], v[18:19], 3, s[48:49]
	global_store_dwordx2 v[18:19], v[44:45], off
	v_add_u32_e32 v18, 0x1200, v14
	v_ashrrev_i32_e32 v19, 31, v18
	v_lshl_add_u64 v[18:19], v[18:19], 3, s[48:49]
	global_store_dwordx2 v[18:19], v[30:31], off
	v_add_u32_e32 v18, 0x1400, v14
	v_ashrrev_i32_e32 v19, 31, v18
	v_lshl_add_u64 v[18:19], v[18:19], 3, s[48:49]
	global_store_dwordx2 v[18:19], v[42:43], off
	v_add_u32_e32 v18, 0x1600, v14
	v_ashrrev_i32_e32 v19, 31, v18
	v_lshl_add_u64 v[18:19], v[18:19], 3, s[48:49]
	global_store_dwordx2 v[18:19], v[28:29], off
	v_add_u32_e32 v18, 0x1800, v14
	v_ashrrev_i32_e32 v19, 31, v18
	v_lshl_add_u64 v[18:19], v[18:19], 3, s[48:49]
	global_store_dwordx2 v[18:19], v[32:33], off
	v_add_u32_e32 v18, 0x1a00, v14
	v_ashrrev_i32_e32 v19, 31, v18
	v_lshl_add_u64 v[18:19], v[18:19], 3, s[48:49]
	global_store_dwordx2 v[18:19], v[26:27], off
	v_add_u32_e32 v18, 0x1c00, v14
	v_ashrrev_i32_e32 v19, 31, v18
	v_lshl_add_u64 v[18:19], v[18:19], 3, s[48:49]
	global_store_dwordx2 v[18:19], v[36:37], off
	v_add_u32_e32 v18, 0x1e00, v14
	v_ashrrev_i32_e32 v19, 31, v18
	v_lshl_add_u64 v[18:19], v[18:19], 3, s[48:49]
	global_store_dwordx2 v[18:19], v[16:17], off
	v_mov_b32_e32 v50, v170
	v_xor_b32_e32 v16, 1, v13
	v_lshlrev_b32_e32 v10, 3, v10
	v_lshlrev_b32_e32 v16, 3, v16
	v_add3_u32 v18, 0, v16, v10
	v_xor_b32_e32 v16, 2, v13
	v_lshlrev_b32_e32 v16, 3, v16
	v_xor_b32_e32 v24, 5, v13
	v_add3_u32 v20, 0, v16, v10
	v_xor_b32_e32 v16, 3, v13
	v_lshlrev_b32_e32 v24, 3, v24
	v_lshlrev_b32_e32 v15, 3, v13
	v_lshlrev_b32_e32 v16, 3, v16
	v_add3_u32 v26, 0, v24, v10
	v_xor_b32_e32 v24, 6, v13
	v_add3_u32 v15, 0, v15, v10
	v_add3_u32 v22, 0, v16, v10
	v_lshlrev_b32_e32 v24, 3, v24
	v_xor_b32_e32 v32, 9, v13
	ds_read_b64 v[16:17], v15
	ds_read_b64 v[18:19], v18
	ds_read_b64 v[20:21], v20
	ds_read_b64 v[22:23], v22
	v_xor_b32_e32 v15, 4, v13
	v_add3_u32 v28, 0, v24, v10
	v_xor_b32_e32 v24, 7, v13
	v_lshlrev_b32_e32 v32, 3, v32
	v_lshlrev_b32_e32 v15, 3, v15
	v_lshlrev_b32_e32 v24, 3, v24
	v_add3_u32 v34, 0, v32, v10
	v_xor_b32_e32 v32, 10, v13
	v_add3_u32 v15, 0, v15, v10
	v_add3_u32 v30, 0, v24, v10
	v_lshlrev_b32_e32 v32, 3, v32
	ds_read_b64 v[24:25], v15
	ds_read_b64 v[26:27], v26
	ds_read_b64 v[28:29], v28
	ds_read_b64 v[30:31], v30
	v_xor_b32_e32 v15, 8, v13
	v_add3_u32 v36, 0, v32, v10
	v_xor_b32_e32 v32, 11, v13
	v_lshlrev_b32_e32 v15, 3, v15
	v_lshlrev_b32_e32 v32, 3, v32
	v_xor_b32_e32 v40, 13, v13
	v_add3_u32 v15, 0, v15, v10
	v_add3_u32 v38, 0, v32, v10
	v_lshlrev_b32_e32 v40, 3, v40
	ds_read_b64 v[32:33], v15
	ds_read_b64 v[34:35], v34
	ds_read_b64 v[36:37], v36
	ds_read_b64 v[38:39], v38
	v_xor_b32_e32 v15, 12, v13
	v_add3_u32 v42, 0, v40, v10
	v_xor_b32_e32 v40, 14, v13
	v_xor_b32_e32 v13, 15, v13
	v_lshlrev_b32_e32 v15, 3, v15
	v_lshlrev_b32_e32 v40, 3, v40
	v_lshlrev_b32_e32 v13, 3, v13
	v_add3_u32 v15, 0, v15, v10
	v_add3_u32 v44, 0, v40, v10
	v_add3_u32 v10, 0, v13, v10
	ds_read_b64 v[40:41], v15
	ds_read_b64 v[42:43], v42
	ds_read_b64 v[44:45], v44
	ds_read_b64 v[46:47], v10
	v_mov_b32_e32 v10, v164
	v_mov_b32_e32 v13, v167
	v_mov_b32_e32 v10, v165
	s_waitcnt lgkmcnt(7)
	v_pk_add_f32 v[52:53], v[16:17], v[32:33]
	v_mov_b32_e32 v10, v166
	v_pk_add_f32 v[16:17], v[16:17], v[32:33] neg_lo:[0,1] neg_hi:[0,1]
	s_waitcnt lgkmcnt(6)
	v_pk_add_f32 v[32:33], v[18:19], v[34:35]
	v_pk_add_f32 v[18:19], v[18:19], v[34:35] neg_lo:[0,1] neg_hi:[0,1]
	v_mov_b32_e32 v13, v169
	s_nop 0
	v_pk_mul_f32 v[34:35], v[18:19], v[50:51] op_sel:[1,0] op_sel_hi:[0,0] neg_lo:[1,1] neg_hi:[0,1]
	v_mov_b32_e32 v13, v171
	v_pk_fma_f32 v[18:19], v[18:19], v[10:11], v[34:35] op_sel_hi:[1,0,1]
	s_waitcnt lgkmcnt(5)
	v_pk_add_f32 v[34:35], v[20:21], v[36:37]
	v_pk_add_f32 v[20:21], v[20:21], v[36:37] neg_lo:[0,1] neg_hi:[0,1]
	s_nop 0
	v_pk_mul_f32 v[36:37], v[20:21], v[48:49] op_sel:[1,0] op_sel_hi:[0,0] neg_lo:[1,1] neg_hi:[0,1]
	v_mov_b32_e32 v13, v172
	v_pk_fma_f32 v[20:21], v[20:21], v[48:49], v[36:37] op_sel_hi:[1,0,1]
	s_waitcnt lgkmcnt(4)
	v_pk_add_f32 v[36:37], v[22:23], v[38:39]
	v_pk_add_f32 v[22:23], v[22:23], v[38:39] neg_lo:[0,1] neg_hi:[0,1]
	s_nop 0
	v_pk_mul_f32 v[38:39], v[22:23], v[50:51] op_sel_hi:[1,0]
	s_nop 0
	v_pk_fma_f32 v[22:23], v[22:23], v[10:11], v[38:39] op_sel:[1,0,0] op_sel_hi:[0,0,1] neg_lo:[1,1,0] neg_hi:[0,1,0]
	s_waitcnt lgkmcnt(3)
	v_pk_add_f32 v[38:39], v[24:25], v[40:41]
	v_pk_add_f32 v[24:25], v[24:25], v[40:41] neg_lo:[0,1] neg_hi:[0,1]
	v_mov_b32_e32 v13, v174
	v_xor_b32_e32 v41, 0x80000000, v24
	v_mov_b32_e32 v40, v25
	s_waitcnt lgkmcnt(2)
	v_pk_add_f32 v[24:25], v[26:27], v[42:43]
	v_pk_add_f32 v[26:27], v[26:27], v[42:43] neg_lo:[0,1] neg_hi:[0,1]
	s_nop 0
	v_pk_mul_f32 v[42:43], v[26:27], v[50:51] op_sel_hi:[1,0] neg_lo:[0,1] neg_hi:[0,1]
	s_nop 0
	v_pk_fma_f32 v[26:27], v[26:27], v[10:11], v[42:43] op_sel:[1,0,0] op_sel_hi:[0,0,1] neg_lo:[1,1,0] neg_hi:[0,1,0]
	s_waitcnt lgkmcnt(1)
	v_pk_add_f32 v[42:43], v[28:29], v[44:45]
	v_pk_add_f32 v[28:29], v[28:29], v[44:45] neg_lo:[0,1] neg_hi:[0,1]
	s_nop 0
	v_pk_mul_f32 v[44:45], v[28:29], v[48:49] op_sel:[1,0] op_sel_hi:[0,0] neg_lo:[1,1] neg_hi:[0,1]
	s_nop 0
	v_pk_fma_f32 v[28:29], v[28:29], v[48:49], v[44:45] op_sel_hi:[1,0,1] neg_lo:[0,1,0] neg_hi:[0,1,0]
	s_waitcnt lgkmcnt(0)
	v_pk_add_f32 v[44:45], v[30:31], v[46:47]
	v_pk_add_f32 v[30:31], v[30:31], v[46:47] neg_lo:[0,1] neg_hi:[0,1]
	s_nop 0
	v_pk_mul_f32 v[46:47], v[30:31], v[50:51] op_sel:[1,0] op_sel_hi:[0,0] neg_lo:[1,1] neg_hi:[0,1]
	v_pk_add_f32 v[50:51], v[32:33], v[24:25]
	v_pk_add_f32 v[24:25], v[32:33], v[24:25] neg_lo:[0,1] neg_hi:[0,1]
	v_pk_fma_f32 v[30:31], v[30:31], v[10:11], v[46:47] op_sel_hi:[1,0,1] neg_lo:[0,1,0] neg_hi:[0,1,0]
	v_pk_mul_f32 v[32:33], v[24:25], v[48:49] op_sel:[1,0] op_sel_hi:[0,0] neg_lo:[1,1] neg_hi:[0,1]
	v_pk_add_f32 v[46:47], v[52:53], v[38:39]
	v_pk_fma_f32 v[24:25], v[24:25], v[48:49], v[32:33] op_sel_hi:[1,0,1]
	v_pk_add_f32 v[32:33], v[34:35], v[42:43]
	v_pk_add_f32 v[34:35], v[34:35], v[42:43] neg_lo:[0,1] neg_hi:[0,1]
	v_pk_add_f32 v[38:39], v[52:53], v[38:39] neg_lo:[0,1] neg_hi:[0,1]
	v_xor_b32_e32 v43, 0x80000000, v34
	v_mov_b32_e32 v42, v35
	v_pk_add_f32 v[34:35], v[36:37], v[44:45]
	v_pk_add_f32 v[36:37], v[36:37], v[44:45] neg_lo:[0,1] neg_hi:[0,1]
	v_mov_b32_e32 v10, v184
	v_pk_mul_f32 v[44:45], v[36:37], v[48:49] op_sel:[1,0] op_sel_hi:[0,0] neg_lo:[1,1] neg_hi:[0,1]
	s_nop 0
	v_pk_fma_f32 v[36:37], v[36:37], v[48:49], v[44:45] op_sel_hi:[1,0,1] neg_lo:[0,1,0] neg_hi:[0,1,0]
	v_pk_add_f32 v[44:45], v[46:47], v[32:33]
	v_pk_add_f32 v[32:33], v[46:47], v[32:33] neg_lo:[0,1] neg_hi:[0,1]
	v_pk_add_f32 v[46:47], v[50:51], v[34:35]
	v_pk_add_f32 v[34:35], v[50:51], v[34:35] neg_lo:[0,1] neg_hi:[0,1]
	s_nop 0
	v_xor_b32_e32 v51, 0x80000000, v34
	v_mov_b32_e32 v50, v35
	v_pk_add_f32 v[34:35], v[44:45], v[46:47]
	v_pk_add_f32 v[44:45], v[44:45], v[46:47] neg_lo:[0,1] neg_hi:[0,1]
	v_pk_add_f32 v[46:47], v[32:33], v[50:51]
	v_pk_add_f32 v[32:33], v[32:33], v[50:51] neg_lo:[0,1] neg_hi:[0,1]
	v_pk_add_f32 v[50:51], v[38:39], v[42:43]
	v_pk_add_f32 v[38:39], v[38:39], v[42:43] neg_lo:[0,1] neg_hi:[0,1]
	v_pk_add_f32 v[42:43], v[24:25], v[36:37]
	v_pk_add_f32 v[24:25], v[24:25], v[36:37] neg_lo:[0,1] neg_hi:[0,1]
	s_nop 0
	v_xor_b32_e32 v37, 0x80000000, v24
	v_mov_b32_e32 v36, v25
	v_pk_add_f32 v[24:25], v[50:51], v[42:43]
	v_pk_add_f32 v[42:43], v[50:51], v[42:43] neg_lo:[0,1] neg_hi:[0,1]
	v_pk_add_f32 v[50:51], v[38:39], v[36:37]
	v_pk_add_f32 v[36:37], v[38:39], v[36:37] neg_lo:[0,1] neg_hi:[0,1]
	v_pk_add_f32 v[38:39], v[16:17], v[40:41]
	v_pk_add_f32 v[16:17], v[16:17], v[40:41] neg_lo:[0,1] neg_hi:[0,1]
	v_pk_add_f32 v[40:41], v[18:19], v[26:27]
	v_pk_add_f32 v[18:19], v[18:19], v[26:27] neg_lo:[0,1] neg_hi:[0,1]
	s_nop 0
	v_pk_mul_f32 v[26:27], v[48:49], v[18:19] op_sel:[0,1] op_sel_hi:[0,0] neg_lo:[1,1] neg_hi:[1,0]
	v_pk_fma_f32 v[18:19], v[48:49], v[18:19], v[26:27] op_sel_hi:[0,1,1]
	v_pk_add_f32 v[26:27], v[20:21], v[28:29]
	v_pk_add_f32 v[20:21], v[20:21], v[28:29] neg_lo:[0,1] neg_hi:[0,1]
	s_nop 0
	v_xor_b32_e32 v29, 0x80000000, v20
	v_mov_b32_e32 v28, v21
	v_pk_add_f32 v[20:21], v[22:23], v[30:31]
	v_pk_add_f32 v[22:23], v[22:23], v[30:31] neg_lo:[0,1] neg_hi:[0,1]
	s_nop 0
	v_pk_mul_f32 v[30:31], v[48:49], v[22:23] op_sel:[0,1] op_sel_hi:[0,0] neg_lo:[1,1] neg_hi:[1,0]
	v_pk_fma_f32 v[22:23], v[48:49], v[22:23], v[30:31] op_sel_hi:[0,1,1] neg_lo:[1,0,0] neg_hi:[1,0,0]
	v_pk_add_f32 v[30:31], v[38:39], v[26:27]
	v_pk_add_f32 v[26:27], v[38:39], v[26:27] neg_lo:[0,1] neg_hi:[0,1]
	v_pk_add_f32 v[38:39], v[40:41], v[20:21]
	v_pk_add_f32 v[20:21], v[40:41], v[20:21] neg_lo:[0,1] neg_hi:[0,1]
	s_nop 0
	v_xor_b32_e32 v41, 0x80000000, v20
	v_mov_b32_e32 v40, v21
	v_pk_add_f32 v[20:21], v[30:31], v[38:39]
	v_pk_add_f32 v[30:31], v[30:31], v[38:39] neg_lo:[0,1] neg_hi:[0,1]
	v_pk_add_f32 v[38:39], v[26:27], v[40:41]
	v_pk_add_f32 v[26:27], v[26:27], v[40:41] neg_lo:[0,1] neg_hi:[0,1]
	v_pk_add_f32 v[40:41], v[16:17], v[28:29]
	v_pk_add_f32 v[16:17], v[16:17], v[28:29] neg_lo:[0,1] neg_hi:[0,1]
	v_pk_add_f32 v[28:29], v[18:19], v[22:23]
	v_pk_add_f32 v[18:19], v[18:19], v[22:23] neg_lo:[0,1] neg_hi:[0,1]
	s_nop 0
	v_xor_b32_e32 v23, 0x80000000, v18
	v_mov_b32_e32 v22, v19
	v_pk_add_f32 v[18:19], v[40:41], v[28:29]
	v_pk_add_f32 v[28:29], v[40:41], v[28:29] neg_lo:[0,1] neg_hi:[0,1]
	v_pk_add_f32 v[40:41], v[16:17], v[22:23]
	v_pk_add_f32 v[16:17], v[16:17], v[22:23] neg_lo:[0,1] neg_hi:[0,1]
	v_add_u32_e32 v22, 0x2000, v14
	v_ashrrev_i32_e32 v23, 31, v22
	v_lshl_add_u64 v[22:23], v[22:23], 3, s[48:49]
	global_store_dwordx2 v[22:23], v[34:35], off
	v_add_u32_e32 v22, 0x2200, v14
	v_ashrrev_i32_e32 v23, 31, v22
	v_lshl_add_u64 v[22:23], v[22:23], 3, s[48:49]
	global_store_dwordx2 v[22:23], v[20:21], off
	v_add_u32_e32 v20, 0x2400, v14
	v_ashrrev_i32_e32 v21, 31, v20
	v_lshl_add_u64 v[20:21], v[20:21], 3, s[48:49]
	global_store_dwordx2 v[20:21], v[24:25], off
	v_add_u32_e32 v20, 0x2600, v14
	v_ashrrev_i32_e32 v21, 31, v20
	v_lshl_add_u64 v[20:21], v[20:21], 3, s[48:49]
	global_store_dwordx2 v[20:21], v[18:19], off
	v_add_u32_e32 v18, 0x2800, v14
	v_ashrrev_i32_e32 v19, 31, v18
	v_lshl_add_u64 v[18:19], v[18:19], 3, s[48:49]
	global_store_dwordx2 v[18:19], v[46:47], off
	v_add_u32_e32 v18, 0x2a00, v14
	v_ashrrev_i32_e32 v19, 31, v18
	v_lshl_add_u64 v[18:19], v[18:19], 3, s[48:49]
	global_store_dwordx2 v[18:19], v[38:39], off
	v_add_u32_e32 v18, 0x2c00, v14
	v_ashrrev_i32_e32 v19, 31, v18
	v_lshl_add_u64 v[18:19], v[18:19], 3, s[48:49]
	global_store_dwordx2 v[18:19], v[50:51], off
	v_add_u32_e32 v18, 0x2e00, v14
	v_ashrrev_i32_e32 v19, 31, v18
	v_lshl_add_u64 v[18:19], v[18:19], 3, s[48:49]
	global_store_dwordx2 v[18:19], v[40:41], off
	v_add_u32_e32 v18, 0x3000, v14
	v_ashrrev_i32_e32 v19, 31, v18
	v_lshl_add_u64 v[18:19], v[18:19], 3, s[48:49]
	global_store_dwordx2 v[18:19], v[44:45], off
	v_add_u32_e32 v18, 0x3200, v14
	v_ashrrev_i32_e32 v19, 31, v18
	v_lshl_add_u64 v[18:19], v[18:19], 3, s[48:49]
	global_store_dwordx2 v[18:19], v[30:31], off
	v_add_u32_e32 v18, 0x3400, v14
	v_ashrrev_i32_e32 v19, 31, v18
	v_lshl_add_u64 v[18:19], v[18:19], 3, s[48:49]
	global_store_dwordx2 v[18:19], v[42:43], off
	v_add_u32_e32 v18, 0x3600, v14
	v_ashrrev_i32_e32 v19, 31, v18
	v_lshl_add_u64 v[18:19], v[18:19], 3, s[48:49]
	global_store_dwordx2 v[18:19], v[28:29], off
	v_add_u32_e32 v18, 0x3800, v14
	v_ashrrev_i32_e32 v19, 31, v18
	v_lshl_add_u64 v[18:19], v[18:19], 3, s[48:49]
	global_store_dwordx2 v[18:19], v[32:33], off
	v_add_u32_e32 v18, 0x3a00, v14
	v_ashrrev_i32_e32 v19, 31, v18
	v_lshl_add_u64 v[18:19], v[18:19], 3, s[48:49]
	global_store_dwordx2 v[18:19], v[26:27], off
	v_add_u32_e32 v18, 0x3c00, v14
	v_add_u32_e32 v14, 0x3e00, v14
	v_ashrrev_i32_e32 v15, 31, v14
	v_ashrrev_i32_e32 v19, 31, v18
	v_lshl_add_u64 v[14:15], v[14:15], 3, s[48:49]
	v_lshl_add_u64 v[18:19], v[18:19], 3, s[48:49]
	global_store_dwordx2 v[14:15], v[16:17], off
	v_mov_b32_e32 v16, v185
	v_mov_b32_e32 v14, v1
	global_store_dwordx2 v[18:19], v[36:37], off
	s_barrier
	s_nop 0
	v_pk_mul_f32 v[36:37], v[16:17], s[66:67] op_sel_hi:[0,1] neg_lo:[1,0]
	s_mov_b64 s[66:67], vcc
	v_ashrrev_i32_e32 v15, 31, v14
	v_lshl_add_u64 v[18:19], v[14:15], 2, s[66:67]
	v_add_co_u32_e32 v28, vcc, s85, v18
	v_pk_mul_f32 v[52:53], v[16:17], s[60:61] op_sel_hi:[0,1] neg_lo:[1,0]
	s_nop 0
	v_addc_co_u32_e32 v29, vcc, 0, v19, vcc
	v_add_co_u32_e32 v20, vcc, s84, v18
	s_movk_i32 s61, 0x3000
	s_nop 0
	v_addc_co_u32_e32 v21, vcc, 0, v19, vcc
	v_add_co_u32_e32 v48, vcc, s61, v18
	v_pk_mul_f32 v[54:55], v[16:17], s[94:95] op_sel_hi:[0,1] neg_lo:[1,0]
	s_nop 0
	v_addc_co_u32_e32 v49, vcc, 0, v19, vcc
	v_add_co_u32_e32 v22, vcc, s45, v18
	v_pk_mul_f32 v[82:83], v[16:17], s[68:69] op_sel_hi:[0,1] neg_lo:[1,0]
	s_nop 0
	v_addc_co_u32_e32 v23, vcc, 0, v19, vcc
	v_add_co_u32_e32 v58, vcc, s86, v18
	s_mov_b32 s68, 0x3f7ec46d
	s_nop 0
	v_addc_co_u32_e32 v59, vcc, 0, v19, vcc
	v_add_co_u32_e32 v60, vcc, s88, v18
	v_pk_mul_f32 v[32:33], v[16:17], s[78:79] op_sel_hi:[0,1] neg_lo:[1,0]
	s_nop 0
	v_addc_co_u32_e32 v61, vcc, 0, v19, vcc
	v_add_co_u32_e32 v66, vcc, s90, v18
	v_pk_mul_f32 v[40:41], v[16:17], s[80:81] op_sel_hi:[0,1] neg_lo:[1,0]
	s_nop 0
	v_addc_co_u32_e32 v67, vcc, 0, v19, vcc
	v_add_co_u32_e32 v68, vcc, s39, v18
	s_mov_b32 s39, 0x9000
	s_nop 0
	v_addc_co_u32_e32 v69, vcc, 0, v19, vcc
	v_add_co_u32_e32 v24, vcc, s39, v18
	s_mov_b32 s39, 0xb000
	s_nop 0
	v_addc_co_u32_e32 v25, vcc, 0, v19, vcc
	v_add_co_u32_e32 v26, vcc, s91, v18
	s_mov_b32 s80, 0x3f54db31
	s_nop 0
	v_addc_co_u32_e32 v27, vcc, 0, v19, vcc
	v_add_co_u32_e32 v34, vcc, s39, v18
	s_mov_b32 s39, 0xc000
	s_nop 0
	v_addc_co_u32_e32 v35, vcc, 0, v19, vcc
	v_add_co_u32_e32 v38, vcc, s39, v18
	s_mov_b32 s39, 0xd000
	s_nop 0
	v_addc_co_u32_e32 v39, vcc, 0, v19, vcc
	v_add_co_u32_e32 v46, vcc, s39, v18
	s_mov_b32 s39, 0xe000
	s_nop 0
	v_addc_co_u32_e32 v47, vcc, 0, v19, vcc
	v_add_co_u32_e32 v50, vcc, s39, v18
	s_mov_b32 s39, 0xf000
	s_nop 0
	v_addc_co_u32_e32 v51, vcc, 0, v19, vcc
	v_add_co_u32_e32 v70, vcc, s39, v18
	s_mov_b32 s69, 0xbdc8bd36
	s_nop 0
	v_addc_co_u32_e32 v71, vcc, 0, v19, vcc
	global_load_dword v90, v[68:69], off
	global_load_dword v92, v[68:69], off offset:2048
	global_load_dword v94, v[26:27], off offset:-4096
	global_load_dword v96, v[24:25], off offset:2048
	global_load_dword v98, v[26:27], off
	global_load_dword v100, v[26:27], off offset:2048
	global_load_dword v102, v[38:39], off offset:-4096
	global_load_dword v104, v[34:35], off offset:2048
	global_load_dword v106, v[38:39], off
	global_load_dword v108, v[38:39], off offset:2048
	global_load_dword v110, v[50:51], off offset:-4096
	global_load_dword v112, v[46:47], off offset:2048
	global_load_dword v114, v[50:51], off
	global_load_dword v116, v[50:51], off offset:2048
	global_load_dword v118, v[70:71], off
	global_load_dword v56, v[20:21], off
	s_nop 0
	global_load_dword v50, v[20:21], off offset:2048
	global_load_dword v120, v[70:71], off offset:2048
	global_load_dword v46, v[22:23], off offset:-4096
	global_load_dword v38, v[22:23], off
	global_load_dword v74, v[20:21], off offset:-4096
	global_load_dword v34, v[22:23], off offset:2048
	global_load_dword v26, v[60:61], off offset:-4096
	global_load_dword v24, v[60:61], off
	s_nop 0
	global_load_dword v22, v[60:61], off offset:2048
	global_load_dword v20, v[68:69], off offset:-4096
	s_nop 0
	global_load_dword v68, v[18:19], off
	global_load_dword v76, v[18:19], off offset:2048
	global_load_dword v72, v[28:29], off offset:2048
	s_nop 0
	global_load_dword v48, v[48:49], off offset:2048
	s_nop 0
	global_load_dword v28, v[58:59], off offset:2048
	global_load_dword v18, v[66:67], off offset:2048
	s_mov_b32 s88, 0x3e47c5c2
	v_pk_fma_f32 v[58:59], v[10:11], s[74:75], v[54:55] op_sel_hi:[0,1,1]
	s_mov_b32 s74, 0x3f226799
	s_mov_b32 s81, 0xbf0e39da
	v_pk_mul_f32 v[42:43], v[16:17], s[52:53] op_sel_hi:[0,1] neg_lo:[1,0]
	v_pk_mul_f32 v[64:65], v[16:17], s[62:63] op_sel_hi:[0,1] neg_lo:[1,0]
	s_mov_b32 s89, 0xbf7b14be
	v_pk_fma_f32 v[124:125], v[10:11], s[68:69], v[32:33] op_sel_hi:[0,1,1]
	s_mov_b32 s75, 0xbf45e403
	s_mov_b32 s52, 0x3f3504f3
	v_pk_mul_f32 v[32:33], v[16:17], s[30:31] op_sel_hi:[0,1] neg_lo:[1,0]
	s_mov_b32 s30, 0x3dc8bd36
	v_pk_mul_f32 v[62:63], v[16:17], s[56:57] op_sel_hi:[0,1] neg_lo:[1,0]
	v_pk_fma_f32 v[60:61], v[10:11], s[80:81], v[52:53] op_sel_hi:[0,1,1]
	s_mov_b32 s53, 0xbf3504f3
	v_pk_fma_f32 v[52:53], v[10:11], s[74:75], v[64:65] op_sel_hi:[0,1,1]
	s_mov_b32 s31, 0xbf7ec46d
	v_pk_fma_f32 v[64:65], v[10:11], s[88:89], v[32:33] op_sel_hi:[0,1,1]
	v_pk_mul_f32 v[32:33], v[16:17], s[34:35] op_sel_hi:[0,1] neg_lo:[1,0]
	s_mov_b32 s78, 0x3f61c598
	v_pk_fma_f32 v[54:55], v[10:11], s[52:53], v[62:63] op_sel_hi:[0,1,1]
	v_pk_fma_f32 v[62:63], v[10:11], s[30:31], v[32:33] op_sel_hi:[0,1,1]
	v_pk_mul_f32 v[32:33], v[16:17], s[36:37] op_sel_hi:[0,1] neg_lo:[1,0]
	s_mov_b32 s79, 0xbef15aea
	v_pk_mul_f32 v[44:45], v[16:17], s[50:51] op_sel_hi:[0,1] neg_lo:[1,0]
	v_pk_fma_f32 v[32:33], v[10:11], s[76:77], v[32:33] op_sel_hi:[0,1,1]
	s_mov_b32 s94, 0x3f6c835e
	v_pk_fma_f32 v[66:67], v[10:11], s[78:79], v[44:45] op_sel_hi:[0,1,1]
	v_pk_fma_f32 v[44:45], v[10:11], s[82:83], v[82:83] op_sel_hi:[0,1,1]
	s_mov_b32 s82, 0x3ef15aea
	s_mov_b32 s95, 0xbec3ef15
	v_pk_mul_f32 v[84:85], v[16:17], s[70:71] op_sel_hi:[0,1] neg_lo:[1,0]
	s_mov_b32 s83, 0xbf61c598
	v_pk_mul_f32 v[30:31], v[16:17], s[40:41] op_sel_hi:[0,1] neg_lo:[1,0]
	s_mov_b32 s84, 0x3ec3ef15
	s_mov_b32 s40, 0x3f74fa0b
	v_pk_fma_f32 v[70:71], v[10:11], s[94:95], v[42:43] op_sel_hi:[0,1,1]
	v_pk_fma_f32 v[42:43], v[10:11], s[82:83], v[84:85] op_sel_hi:[0,1,1]
	s_mov_b32 s85, 0xbf6c835e
	s_mov_b32 s41, 0xbe94a031
	v_pk_mul_f32 v[86:87], v[16:17], s[58:59] op_sel_hi:[0,1] neg_lo:[1,0]
	s_mov_b32 s86, 0x3e94a031
	v_pk_fma_f32 v[78:79], v[10:11], s[40:41], v[40:41] op_sel_hi:[0,1,1]
	v_pk_fma_f32 v[40:41], v[10:11], s[84:85], v[86:87] op_sel_hi:[0,1,1]
	s_mov_b32 s87, 0xbf74fa0b
	v_pk_mul_f32 v[88:89], v[16:17], s[64:65] op_sel_hi:[0,1] neg_lo:[1,0]
	v_pk_fma_f32 v[122:123], v[10:11], s[46:47], v[30:31] op_sel_hi:[0,1,1]
	v_pk_fma_f32 v[30:31], v[10:11], s[86:87], v[88:89] op_sel_hi:[0,1,1]
	s_waitcnt vmcnt(31)
	v_pk_mul_f32 v[82:83], v[32:33], v[90:91] op_sel_hi:[1,0]
	v_pk_mul_f32 v[32:33], v[16:17], s[2:3] op_sel_hi:[0,1] neg_lo:[1,0]
	v_pk_fma_f32 v[32:33], v[10:11], s[0:1], v[32:33] op_sel_hi:[0,1,1]
	s_waitcnt vmcnt(30)
	v_pk_mul_f32 v[84:85], v[32:33], v[92:93] op_sel_hi:[1,0]
	v_pk_mul_f32 v[32:33], v[16:17], s[6:7] op_sel_hi:[0,1] neg_lo:[1,0]
	v_pk_fma_f32 v[32:33], v[10:11], s[4:5], v[32:33] op_sel_hi:[0,1,1]
	s_waitcnt vmcnt(29)
	v_pk_mul_f32 v[86:87], v[32:33], v[94:95] op_sel_hi:[1,0]
	v_pk_mul_f32 v[32:33], v[16:17], s[10:11] op_sel_hi:[0,1] neg_lo:[1,0]
	v_pk_fma_f32 v[32:33], v[10:11], s[8:9], v[32:33] op_sel_hi:[0,1,1]
	s_waitcnt vmcnt(28)
	v_pk_mul_f32 v[88:89], v[32:33], v[96:97] op_sel_hi:[1,0]
	v_pk_mul_f32 v[32:33], v[16:17], s[16:17] op_sel_hi:[0,1] neg_lo:[1,0]
	v_pk_fma_f32 v[32:33], v[10:11], s[12:13], v[32:33] op_sel_hi:[0,1,1]
	s_waitcnt vmcnt(27)
	v_pk_mul_f32 v[90:91], v[32:33], v[98:99] op_sel_hi:[1,0]
	v_pk_mul_f32 v[32:33], v[16:17], s[20:21] op_sel_hi:[0,1] neg_lo:[1,0]
	v_pk_fma_f32 v[32:33], v[10:11], s[18:19], v[32:33] op_sel_hi:[0,1,1]
	s_waitcnt vmcnt(26)
	v_pk_mul_f32 v[92:93], v[32:33], v[100:101] op_sel_hi:[1,0]
	v_pk_mul_f32 v[32:33], v[16:17], s[24:25] op_sel_hi:[0,1] neg_lo:[1,0]
	v_pk_fma_f32 v[32:33], v[10:11], s[22:23], v[32:33] op_sel_hi:[0,1,1]
	s_waitcnt vmcnt(25)
	v_pk_mul_f32 v[94:95], v[32:33], v[102:103] op_sel_hi:[1,0]
	v_pk_mul_f32 v[32:33], v[16:17], s[28:29] op_sel_hi:[0,1] neg_lo:[1,0]
	v_pk_fma_f32 v[32:33], v[10:11], s[26:27], v[32:33] op_sel_hi:[0,1,1]
	s_waitcnt vmcnt(24)
	v_pk_mul_f32 v[96:97], v[32:33], v[104:105] op_sel_hi:[1,0]
	v_pk_mul_f32 v[32:33], v[16:17], s[52:53] op_sel_hi:[0,0] neg_lo:[1,0]
	v_pk_fma_f32 v[32:33], v[10:11], s[38:39], v[32:33] op_sel_hi:[0,0,1] neg_lo:[0,0,1] neg_hi:[0,0,1]
	s_waitcnt vmcnt(23)
	v_pk_mul_f32 v[98:99], v[32:33], v[106:107] op_sel_hi:[1,0]
	v_pk_mul_f32 v[32:33], v[16:17], s[26:27] op_sel_hi:[0,1] neg_lo:[1,0]
	v_pk_fma_f32 v[32:33], v[10:11], s[28:29], v[32:33] op_sel_hi:[0,1,1]
	s_waitcnt vmcnt(22)
	v_pk_mul_f32 v[100:101], v[32:33], v[108:109] op_sel_hi:[1,0]
	v_pk_mul_f32 v[32:33], v[16:17], s[22:23] op_sel_hi:[0,1] neg_lo:[1,0]
	v_pk_fma_f32 v[32:33], v[10:11], s[24:25], v[32:33] op_sel_hi:[0,1,1]
	s_waitcnt vmcnt(21)
	v_pk_mul_f32 v[102:103], v[32:33], v[110:111] op_sel_hi:[1,0]
	v_pk_mul_f32 v[32:33], v[16:17], s[18:19] op_sel_hi:[0,1] neg_lo:[1,0]
	v_pk_fma_f32 v[32:33], v[10:11], s[20:21], v[32:33] op_sel_hi:[0,1,1]
	s_waitcnt vmcnt(20)
	v_pk_mul_f32 v[104:105], v[32:33], v[112:113] op_sel_hi:[1,0]
	v_pk_mul_f32 v[32:33], v[16:17], s[12:13] op_sel_hi:[0,1] neg_lo:[1,0]
	v_pk_fma_f32 v[32:33], v[10:11], s[16:17], v[32:33] op_sel_hi:[0,1,1]
	s_waitcnt vmcnt(19)
	v_pk_mul_f32 v[106:107], v[32:33], v[114:115] op_sel_hi:[1,0]
	v_pk_mul_f32 v[32:33], v[16:17], s[8:9] op_sel_hi:[0,1] neg_lo:[1,0]
	v_pk_fma_f32 v[32:33], v[10:11], s[10:11], v[32:33] op_sel_hi:[0,1,1]
	s_mov_b32 s70, 0x3f7b14be
	s_waitcnt vmcnt(18)
	v_pk_mul_f32 v[108:109], v[32:33], v[116:117] op_sel_hi:[1,0]
	v_pk_mul_f32 v[32:33], v[16:17], s[4:5] op_sel_hi:[0,1] neg_lo:[1,0]
	v_pk_mul_f32 v[16:17], v[16:17], s[0:1] op_sel_hi:[0,1] neg_lo:[1,0]
	s_mov_b32 s71, 0xbe47c5c2
	v_pk_fma_f32 v[16:17], v[10:11], s[2:3], v[16:17] op_sel_hi:[0,1,1]
	v_pk_fma_f32 v[80:81], v[10:11], s[70:71], v[36:37] op_sel_hi:[0,1,1]
	v_pk_fma_f32 v[32:33], v[10:11], s[6:7], v[32:33] op_sel_hi:[0,1,1]
	s_waitcnt vmcnt(14)
	v_pk_mul_f32 v[112:113], v[16:17], v[120:121] op_sel_hi:[1,0]
	v_mov_b32_e32 v10, v164
	s_waitcnt vmcnt(5)
	v_pk_fma_f32 v[126:127], v[68:69], v[122:123], v[82:83] op_sel_hi:[0,1,1]
	v_pk_fma_f32 v[68:69], v[68:69], v[122:123], v[82:83] op_sel_hi:[0,1,1] neg_lo:[0,0,1] neg_hi:[0,0,1]
	s_waitcnt vmcnt(4)
	v_pk_fma_f32 v[82:83], v[124:125], v[76:77], v[84:85] op_sel_hi:[1,0,1]
	v_pk_fma_f32 v[76:77], v[124:125], v[76:77], v[84:85] op_sel_hi:[1,0,1] neg_lo:[0,0,1] neg_hi:[0,0,1]
	v_pk_mul_f32 v[110:111], v[32:33], v[118:119] op_sel_hi:[1,0]
	v_mov_b32_e32 v114, v165
	v_mov_b32_e32 v32, v166
	v_mov_b32_e32 v116, v167
	v_mov_b32_e32 v10, v168
	v_mov_b32_e32 v118, v169
	v_mov_b32_e32 v36, v170
	v_mov_b32_e32 v120, v171
	v_mov_b32_e32 v15, v172
	v_pk_mul_f32 v[84:85], v[76:77], v[120:121] op_sel:[1,0] op_sel_hi:[0,0] neg_lo:[1,1] neg_hi:[0,1]
	s_nop 0
	v_pk_fma_f32 v[76:77], v[76:77], v[114:115], v[84:85] op_sel_hi:[1,0,1]
	v_pk_fma_f32 v[84:85], v[80:81], v[74:75], v[86:87] op_sel_hi:[1,0,1]
	v_pk_fma_f32 v[74:75], v[80:81], v[74:75], v[86:87] op_sel_hi:[1,0,1] neg_lo:[0,0,1] neg_hi:[0,0,1]
	s_nop 0
	v_pk_mul_f32 v[80:81], v[74:75], v[36:37] op_sel:[1,0] op_sel_hi:[0,0] neg_lo:[1,1] neg_hi:[0,1]
	s_nop 0
	v_pk_fma_f32 v[74:75], v[74:75], v[32:33], v[80:81] op_sel_hi:[1,0,1]
	s_waitcnt vmcnt(3)
	v_pk_fma_f32 v[80:81], v[78:79], v[72:73], v[88:89] op_sel_hi:[1,0,1]
	v_pk_fma_f32 v[72:73], v[78:79], v[72:73], v[88:89] op_sel_hi:[1,0,1] neg_lo:[0,0,1] neg_hi:[0,0,1]
	s_nop 0
	v_pk_mul_f32 v[78:79], v[72:73], v[118:119] op_sel:[1,0] op_sel_hi:[0,0] neg_lo:[1,1] neg_hi:[0,1]
	s_nop 0
	v_pk_fma_f32 v[72:73], v[72:73], v[116:117], v[78:79] op_sel_hi:[1,0,1]
	v_pk_fma_f32 v[78:79], v[70:71], v[56:57], v[90:91] op_sel_hi:[1,0,1]
	v_pk_fma_f32 v[56:57], v[70:71], v[56:57], v[90:91] op_sel_hi:[1,0,1] neg_lo:[0,0,1] neg_hi:[0,0,1]
	s_nop 0
	v_pk_mul_f32 v[70:71], v[56:57], v[10:11] op_sel:[1,0] op_sel_hi:[0,0] neg_lo:[1,1] neg_hi:[0,1]
	s_nop 0
	v_pk_fma_f32 v[56:57], v[56:57], v[10:11], v[70:71] op_sel_hi:[1,0,1]
	v_pk_fma_f32 v[70:71], v[66:67], v[50:51], v[92:93] op_sel_hi:[1,0,1]
	v_pk_fma_f32 v[50:51], v[66:67], v[50:51], v[92:93] op_sel_hi:[1,0,1] neg_lo:[0,0,1] neg_hi:[0,0,1]
	s_nop 0
	v_pk_mul_f32 v[66:67], v[50:51], v[118:119] op_sel_hi:[1,0]
	v_xor_b32_e32 v86, 0x80000000, v51
	v_mov_b32_e32 v87, v50
	v_pk_fma_f32 v[50:51], v[60:61], v[46:47], v[94:95] op_sel_hi:[1,0,1]
	v_pk_fma_f32 v[46:47], v[60:61], v[46:47], v[94:95] op_sel_hi:[1,0,1] neg_lo:[0,0,1] neg_hi:[0,0,1]
	v_pk_fma_f32 v[66:67], v[86:87], v[116:117], v[66:67] op_sel_hi:[1,0,1] neg_lo:[0,1,0] neg_hi:[0,1,0]
	v_pk_mul_f32 v[60:61], v[46:47], v[36:37] op_sel_hi:[1,0]
	v_xor_b32_e32 v86, 0x80000000, v47
	v_mov_b32_e32 v87, v46
	s_waitcnt vmcnt(2)
	v_pk_fma_f32 v[46:47], v[58:59], v[48:49], v[96:97] op_sel_hi:[1,0,1]
	v_pk_fma_f32 v[48:49], v[58:59], v[48:49], v[96:97] op_sel_hi:[1,0,1] neg_lo:[0,0,1] neg_hi:[0,0,1]
	v_pk_fma_f32 v[60:61], v[86:87], v[32:33], v[60:61] op_sel_hi:[1,0,1] neg_lo:[0,1,0] neg_hi:[0,1,0]
	v_pk_mul_f32 v[58:59], v[48:49], v[120:121] op_sel_hi:[1,0]
	s_nop 0
	v_pk_fma_f32 v[48:49], v[48:49], v[114:115], v[58:59] op_sel:[1,0,0] op_sel_hi:[0,0,1] neg_lo:[1,1,0] neg_hi:[0,1,0]
	v_pk_fma_f32 v[58:59], v[54:55], v[38:39], v[98:99] op_sel_hi:[1,0,1]
	v_pk_fma_f32 v[38:39], v[54:55], v[38:39], v[98:99] op_sel_hi:[1,0,1] neg_lo:[0,0,1] neg_hi:[0,0,1]
	s_nop 0
	v_xor_b32_e32 v55, 0x80000000, v38
	v_mov_b32_e32 v54, v39
	v_pk_fma_f32 v[38:39], v[52:53], v[34:35], v[100:101] op_sel_hi:[1,0,1]
	v_pk_fma_f32 v[34:35], v[52:53], v[34:35], v[100:101] op_sel_hi:[1,0,1] neg_lo:[0,0,1] neg_hi:[0,0,1]
	s_nop 0
	v_pk_mul_f32 v[52:53], v[34:35], v[120:121] op_sel_hi:[1,0] neg_lo:[0,1] neg_hi:[0,1]
	v_xor_b32_e32 v86, 0x80000000, v35
	v_mov_b32_e32 v87, v34
	v_pk_fma_f32 v[34:35], v[44:45], v[26:27], v[102:103] op_sel_hi:[1,0,1]
	v_pk_fma_f32 v[26:27], v[44:45], v[26:27], v[102:103] op_sel_hi:[1,0,1] neg_lo:[0,0,1] neg_hi:[0,0,1]
	v_pk_fma_f32 v[52:53], v[86:87], v[114:115], v[52:53] op_sel_hi:[1,0,1] neg_lo:[0,1,0] neg_hi:[0,1,0]
	v_pk_mul_f32 v[44:45], v[26:27], v[36:37] op_sel_hi:[1,0] neg_lo:[0,1] neg_hi:[0,1]
	v_xor_b32_e32 v86, 0x80000000, v27
	v_mov_b32_e32 v87, v26
	s_waitcnt vmcnt(1)
	v_pk_fma_f32 v[26:27], v[42:43], v[28:29], v[104:105] op_sel_hi:[1,0,1]
	v_pk_fma_f32 v[28:29], v[42:43], v[28:29], v[104:105] op_sel_hi:[1,0,1] neg_lo:[0,0,1] neg_hi:[0,0,1]
	v_pk_fma_f32 v[86:87], v[86:87], v[32:33], v[44:45] op_sel_hi:[1,0,1] neg_lo:[0,1,0] neg_hi:[0,1,0]
	v_pk_mul_f32 v[42:43], v[28:29], v[118:119] op_sel_hi:[1,0] neg_lo:[0,1] neg_hi:[0,1]
	v_xor_b32_e32 v44, 0x80000000, v29
	v_mov_b32_e32 v45, v28
	v_pk_fma_f32 v[28:29], v[40:41], v[24:25], v[106:107] op_sel_hi:[1,0,1]
	v_pk_fma_f32 v[24:25], v[40:41], v[24:25], v[106:107] op_sel_hi:[1,0,1] neg_lo:[0,0,1] neg_hi:[0,0,1]
	v_pk_fma_f32 v[42:43], v[44:45], v[116:117], v[42:43] op_sel_hi:[1,0,1] neg_lo:[0,1,0] neg_hi:[0,1,0]
	v_pk_mul_f32 v[40:41], v[24:25], v[10:11] op_sel:[1,0] op_sel_hi:[0,0] neg_lo:[1,1] neg_hi:[0,1]
	v_pk_add_f32 v[44:45], v[126:127], v[58:59] neg_lo:[0,1] neg_hi:[0,1]
	v_pk_fma_f32 v[88:89], v[24:25], v[10:11], v[40:41] op_sel_hi:[1,0,1] neg_lo:[0,1,0] neg_hi:[0,1,0]
	v_pk_fma_f32 v[24:25], v[30:31], v[22:23], v[108:109] op_sel_hi:[1,0,1]
	v_pk_fma_f32 v[22:23], v[30:31], v[22:23], v[108:109] op_sel_hi:[1,0,1] neg_lo:[0,0,1] neg_hi:[0,0,1]
	s_nop 0
	v_pk_mul_f32 v[30:31], v[22:23], v[118:119] op_sel:[1,0] op_sel_hi:[0,0] neg_lo:[1,1] neg_hi:[0,1]
	s_nop 0
	v_pk_fma_f32 v[90:91], v[22:23], v[116:117], v[30:31] op_sel_hi:[1,0,1] neg_lo:[0,1,0] neg_hi:[0,1,0]
	v_pk_fma_f32 v[22:23], v[64:65], v[20:21], v[110:111] op_sel_hi:[1,0,1]
	v_pk_fma_f32 v[20:21], v[64:65], v[20:21], v[110:111] op_sel_hi:[1,0,1] neg_lo:[0,0,1] neg_hi:[0,0,1]
	s_nop 0
	v_pk_mul_f32 v[30:31], v[20:21], v[36:37] op_sel:[1,0] op_sel_hi:[0,0] neg_lo:[1,1] neg_hi:[0,1]
	s_nop 0
	v_pk_fma_f32 v[64:65], v[20:21], v[32:33], v[30:31] op_sel_hi:[1,0,1] neg_lo:[0,1,0] neg_hi:[0,1,0]
	s_waitcnt vmcnt(0)
	v_pk_fma_f32 v[20:21], v[62:63], v[18:19], v[112:113] op_sel_hi:[1,0,1]
	v_pk_fma_f32 v[18:19], v[62:63], v[18:19], v[112:113] op_sel_hi:[1,0,1] neg_lo:[0,0,1] neg_hi:[0,0,1]
	s_nop 0
	v_pk_mul_f32 v[30:31], v[18:19], v[120:121] op_sel:[1,0] op_sel_hi:[0,0] neg_lo:[1,1] neg_hi:[0,1]
	s_nop 0
	v_pk_fma_f32 v[62:63], v[18:19], v[114:115], v[30:31] op_sel_hi:[1,0,1] neg_lo:[0,1,0] neg_hi:[0,1,0]
	v_pk_add_f32 v[30:31], v[82:83], v[38:39]
	v_pk_add_f32 v[38:39], v[82:83], v[38:39] neg_lo:[0,1] neg_hi:[0,1]
	v_pk_add_f32 v[18:19], v[126:127], v[58:59]
	v_pk_mul_f32 v[40:41], v[38:39], v[36:37] op_sel:[1,0] op_sel_hi:[0,0] neg_lo:[1,1] neg_hi:[0,1]
	s_nop 0
	v_pk_fma_f32 v[38:39], v[38:39], v[32:33], v[40:41] op_sel_hi:[1,0,1]
	v_pk_add_f32 v[40:41], v[84:85], v[34:35]
	v_pk_add_f32 v[34:35], v[84:85], v[34:35] neg_lo:[0,1] neg_hi:[0,1]
	s_nop 0
	v_pk_mul_f32 v[58:59], v[34:35], v[10:11] op_sel:[1,0] op_sel_hi:[0,0] neg_lo:[1,1] neg_hi:[0,1]
	s_nop 0
	v_pk_fma_f32 v[34:35], v[34:35], v[10:11], v[58:59] op_sel_hi:[1,0,1]
	v_pk_add_f32 v[58:59], v[80:81], v[26:27]
	v_pk_add_f32 v[26:27], v[80:81], v[26:27] neg_lo:[0,1] neg_hi:[0,1]
	s_nop 0
	v_pk_mul_f32 v[80:81], v[26:27], v[36:37] op_sel_hi:[1,0]
	v_xor_b32_e32 v82, 0x80000000, v27
	v_mov_b32_e32 v83, v26
	v_pk_add_f32 v[26:27], v[78:79], v[28:29]
	v_pk_add_f32 v[28:29], v[78:79], v[28:29] neg_lo:[0,1] neg_hi:[0,1]
	v_pk_fma_f32 v[80:81], v[82:83], v[32:33], v[80:81] op_sel_hi:[1,0,1] neg_lo:[0,1,0] neg_hi:[0,1,0]
	v_xor_b32_e32 v79, 0x80000000, v28
	v_mov_b32_e32 v78, v29
	v_pk_add_f32 v[28:29], v[70:71], v[24:25]
	v_pk_add_f32 v[24:25], v[70:71], v[24:25] neg_lo:[0,1] neg_hi:[0,1]
	s_nop 0
	v_pk_mul_f32 v[70:71], v[24:25], v[36:37] op_sel_hi:[1,0] neg_lo:[0,1] neg_hi:[0,1]
	s_nop 0
	v_pk_fma_f32 v[24:25], v[24:25], v[32:33], v[70:71] op_sel:[1,0,0] op_sel_hi:[0,0,1] neg_lo:[1,1,0] neg_hi:[0,1,0]
	v_pk_add_f32 v[70:71], v[50:51], v[22:23]
	v_pk_add_f32 v[22:23], v[50:51], v[22:23] neg_lo:[0,1] neg_hi:[0,1]
	s_nop 0
	v_pk_mul_f32 v[50:51], v[22:23], v[10:11] op_sel:[1,0] op_sel_hi:[0,0] neg_lo:[1,1] neg_hi:[0,1]
	s_nop 0
	v_pk_fma_f32 v[50:51], v[22:23], v[10:11], v[50:51] op_sel_hi:[1,0,1] neg_lo:[0,1,0] neg_hi:[0,1,0]
	v_pk_add_f32 v[22:23], v[46:47], v[20:21]
	v_pk_add_f32 v[20:21], v[46:47], v[20:21] neg_lo:[0,1] neg_hi:[0,1]
	s_nop 0
	v_pk_mul_f32 v[46:47], v[20:21], v[36:37] op_sel:[1,0] op_sel_hi:[0,0] neg_lo:[1,1] neg_hi:[0,1]
	s_nop 0
	v_pk_fma_f32 v[20:21], v[20:21], v[32:33], v[46:47] op_sel_hi:[1,0,1] neg_lo:[0,1,0] neg_hi:[0,1,0]
	v_pk_add_f32 v[46:47], v[18:19], v[26:27]
	v_pk_add_f32 v[18:19], v[18:19], v[26:27] neg_lo:[0,1] neg_hi:[0,1]
	v_pk_add_f32 v[26:27], v[30:31], v[28:29]
	v_pk_add_f32 v[28:29], v[30:31], v[28:29] neg_lo:[0,1] neg_hi:[0,1]
	s_nop 0
	v_pk_mul_f32 v[30:31], v[28:29], v[10:11] op_sel:[1,0] op_sel_hi:[0,0] neg_lo:[1,1] neg_hi:[0,1]
	s_nop 0
	v_pk_fma_f32 v[28:29], v[28:29], v[10:11], v[30:31] op_sel_hi:[1,0,1]
	v_pk_add_f32 v[30:31], v[40:41], v[70:71]
	v_pk_add_f32 v[40:41], v[40:41], v[70:71] neg_lo:[0,1] neg_hi:[0,1]
	v_pk_add_f32 v[82:83], v[46:47], v[30:31] neg_lo:[0,1] neg_hi:[0,1]
	v_xor_b32_e32 v71, 0x80000000, v40
	v_mov_b32_e32 v70, v41
	v_pk_add_f32 v[40:41], v[58:59], v[22:23]
	v_pk_add_f32 v[22:23], v[58:59], v[22:23] neg_lo:[0,1] neg_hi:[0,1]
	s_nop 0
	v_pk_mul_f32 v[58:59], v[22:23], v[10:11] op_sel:[1,0] op_sel_hi:[0,0] neg_lo:[1,1] neg_hi:[0,1]
	s_nop 0
	v_pk_fma_f32 v[58:59], v[22:23], v[10:11], v[58:59] op_sel_hi:[1,0,1] neg_lo:[0,1,0] neg_hi:[0,1,0]
	v_pk_add_f32 v[22:23], v[46:47], v[30:31]
	v_pk_add_f32 v[30:31], v[26:27], v[40:41]
	v_pk_add_f32 v[26:27], v[26:27], v[40:41] neg_lo:[0,1] neg_hi:[0,1]
	v_pk_add_f32 v[84:85], v[22:23], v[30:31]
	v_pk_add_f32 v[30:31], v[22:23], v[30:31] neg_lo:[0,1] neg_hi:[0,1]
	v_pk_add_f32 v[46:47], v[82:83], v[26:27] op_sel:[0,1] op_sel_hi:[1,0] neg_hi:[0,1]
	v_pk_add_f32 v[22:23], v[82:83], v[26:27] op_sel:[0,1] op_sel_hi:[1,0] neg_lo:[0,1]
	v_pk_add_f32 v[40:41], v[28:29], v[58:59]
	v_pk_add_f32 v[28:29], v[28:29], v[58:59] neg_lo:[0,1] neg_hi:[0,1]
	v_pk_add_f32 v[26:27], v[18:19], v[70:71]
	v_pk_add_f32 v[18:19], v[18:19], v[70:71] neg_lo:[0,1] neg_hi:[0,1]
	v_pk_add_f32 v[70:71], v[26:27], v[40:41]
	v_pk_add_f32 v[26:27], v[26:27], v[40:41] neg_lo:[0,1] neg_hi:[0,1]
	v_pk_add_f32 v[40:41], v[18:19], v[28:29] op_sel:[0,1] op_sel_hi:[1,0] neg_hi:[0,1]
	v_pk_add_f32 v[18:19], v[18:19], v[28:29] op_sel:[0,1] op_sel_hi:[1,0] neg_lo:[0,1]
	v_pk_add_f32 v[58:59], v[38:39], v[24:25]
	v_pk_add_f32 v[24:25], v[38:39], v[24:25] neg_lo:[0,1] neg_hi:[0,1]
	v_pk_add_f32 v[28:29], v[44:45], v[78:79]
	v_pk_mul_f32 v[38:39], v[10:11], v[24:25] op_sel:[0,1] op_sel_hi:[0,0] neg_lo:[1,1] neg_hi:[1,0]
	v_pk_fma_f32 v[38:39], v[10:11], v[24:25], v[38:39] op_sel_hi:[0,1,1]
	v_pk_add_f32 v[24:25], v[34:35], v[50:51]
	v_pk_add_f32 v[34:35], v[34:35], v[50:51] neg_lo:[0,1] neg_hi:[0,1]
	v_pk_add_f32 v[44:45], v[44:45], v[78:79] neg_lo:[0,1] neg_hi:[0,1]
	v_xor_b32_e32 v79, 0x80000000, v34
	v_mov_b32_e32 v78, v35
	v_pk_add_f32 v[34:35], v[80:81], v[20:21]
	v_pk_add_f32 v[20:21], v[80:81], v[20:21] neg_lo:[0,1] neg_hi:[0,1]
	s_nop 0
	v_pk_mul_f32 v[50:51], v[10:11], v[20:21] op_sel:[0,1] op_sel_hi:[0,0] neg_lo:[1,1] neg_hi:[1,0]
	v_pk_fma_f32 v[20:21], v[10:11], v[20:21], v[50:51] op_sel_hi:[0,1,1] neg_lo:[1,0,0] neg_hi:[1,0,0]
	v_pk_add_f32 v[50:51], v[28:29], v[24:25]
	v_pk_add_f32 v[24:25], v[28:29], v[24:25] neg_lo:[0,1] neg_hi:[0,1]
	v_pk_add_f32 v[28:29], v[58:59], v[34:35]
	v_pk_add_f32 v[34:35], v[58:59], v[34:35] neg_lo:[0,1] neg_hi:[0,1]
	v_pk_add_f32 v[80:81], v[50:51], v[28:29]
	v_xor_b32_e32 v59, 0x80000000, v34
	v_mov_b32_e32 v58, v35
	v_pk_add_f32 v[34:35], v[50:51], v[28:29] neg_lo:[0,1] neg_hi:[0,1]
	v_pk_add_f32 v[50:51], v[24:25], v[58:59]
	v_pk_add_f32 v[24:25], v[24:25], v[58:59] neg_lo:[0,1] neg_hi:[0,1]
	v_pk_add_f32 v[28:29], v[44:45], v[78:79]
	v_pk_add_f32 v[58:59], v[44:45], v[78:79] neg_lo:[0,1] neg_hi:[0,1]
	v_pk_add_f32 v[44:45], v[38:39], v[20:21]
	v_pk_add_f32 v[20:21], v[38:39], v[20:21] neg_lo:[0,1] neg_hi:[0,1]
	v_pk_add_f32 v[78:79], v[28:29], v[44:45]
	v_pk_add_f32 v[28:29], v[28:29], v[44:45] neg_lo:[0,1] neg_hi:[0,1]
	v_pk_add_f32 v[44:45], v[58:59], v[20:21] op_sel:[0,1] op_sel_hi:[1,0] neg_hi:[0,1]
	v_pk_add_f32 v[20:21], v[58:59], v[20:21] op_sel:[0,1] op_sel_hi:[1,0] neg_lo:[0,1]
	v_pk_add_f32 v[38:39], v[68:69], v[54:55]
	v_pk_add_f32 v[58:59], v[68:69], v[54:55] neg_lo:[0,1] neg_hi:[0,1]
	v_pk_add_f32 v[54:55], v[76:77], v[52:53]
	v_pk_add_f32 v[52:53], v[76:77], v[52:53] neg_lo:[0,1] neg_hi:[0,1]
	s_nop 0
	v_pk_mul_f32 v[68:69], v[36:37], v[52:53] op_sel:[0,1] op_sel_hi:[0,0] neg_lo:[1,1] neg_hi:[1,0]
	v_pk_fma_f32 v[52:53], v[32:33], v[52:53], v[68:69] op_sel_hi:[0,1,1]
	v_pk_add_f32 v[68:69], v[74:75], v[86:87]
	v_pk_add_f32 v[74:75], v[74:75], v[86:87] neg_lo:[0,1] neg_hi:[0,1]
	s_nop 0
	v_pk_mul_f32 v[76:77], v[10:11], v[74:75] op_sel:[0,1] op_sel_hi:[0,0] neg_lo:[1,1] neg_hi:[1,0]
	v_pk_fma_f32 v[74:75], v[10:11], v[74:75], v[76:77] op_sel_hi:[0,1,1]
	v_pk_add_f32 v[76:77], v[72:73], v[42:43]
	v_pk_add_f32 v[42:43], v[72:73], v[42:43] neg_lo:[0,1] neg_hi:[0,1]
	s_nop 0
	v_pk_mul_f32 v[72:73], v[32:33], v[42:43] op_sel:[0,1] op_sel_hi:[0,0] neg_lo:[1,1] neg_hi:[1,0]
	v_pk_fma_f32 v[42:43], v[36:37], v[42:43], v[72:73] op_sel_hi:[0,1,1]
	v_pk_add_f32 v[72:73], v[56:57], v[88:89]
	v_pk_add_f32 v[56:57], v[56:57], v[88:89] neg_lo:[0,1] neg_hi:[0,1]
	s_nop 0
	v_xor_b32_e32 v83, 0x80000000, v56
	v_mov_b32_e32 v82, v57
	v_pk_add_f32 v[56:57], v[66:67], v[90:91]
	v_pk_add_f32 v[66:67], v[66:67], v[90:91] neg_lo:[0,1] neg_hi:[0,1]
	s_nop 0
	v_pk_mul_f32 v[86:87], v[32:33], v[66:67] op_sel:[0,1] op_sel_hi:[0,0] neg_lo:[1,1] neg_hi:[1,0]
	v_pk_fma_f32 v[66:67], v[36:37], v[66:67], v[86:87] op_sel_hi:[0,1,1] neg_lo:[1,0,0] neg_hi:[1,0,0]
	v_pk_add_f32 v[86:87], v[60:61], v[64:65]
	v_pk_add_f32 v[60:61], v[60:61], v[64:65] neg_lo:[0,1] neg_hi:[0,1]
	s_nop 0
	v_pk_mul_f32 v[64:65], v[10:11], v[60:61] op_sel:[0,1] op_sel_hi:[0,0] neg_lo:[1,1] neg_hi:[1,0]
	v_pk_fma_f32 v[60:61], v[10:11], v[60:61], v[64:65] op_sel_hi:[0,1,1] neg_lo:[1,0,0] neg_hi:[1,0,0]
	v_pk_add_f32 v[64:65], v[48:49], v[62:63]
	v_pk_add_f32 v[48:49], v[48:49], v[62:63] neg_lo:[0,1] neg_hi:[0,1]
	s_nop 0
	v_pk_mul_f32 v[36:37], v[36:37], v[48:49] op_sel:[0,1] op_sel_hi:[0,0] neg_lo:[1,1] neg_hi:[1,0]
	v_pk_fma_f32 v[36:37], v[32:33], v[48:49], v[36:37] op_sel_hi:[0,1,1] neg_lo:[1,0,0] neg_hi:[1,0,0]
	v_pk_add_f32 v[32:33], v[38:39], v[72:73]
	v_pk_add_f32 v[48:49], v[38:39], v[72:73] neg_lo:[0,1] neg_hi:[0,1]
	v_pk_add_f32 v[38:39], v[56:57], v[54:55]
	v_pk_add_f32 v[54:55], v[54:55], v[56:57] neg_lo:[0,1] neg_hi:[0,1]
	v_pk_add_f32 v[62:63], v[68:69], v[86:87] neg_lo:[0,1] neg_hi:[0,1]
	v_pk_mul_f32 v[56:57], v[10:11], v[54:55] op_sel:[0,1] op_sel_hi:[0,0] neg_lo:[1,1] neg_hi:[1,0]
	v_pk_fma_f32 v[56:57], v[10:11], v[54:55], v[56:57] op_sel_hi:[0,1,1]
	v_pk_add_f32 v[54:55], v[68:69], v[86:87]
	v_xor_b32_e32 v69, 0x80000000, v62
	v_mov_b32_e32 v68, v63
	v_pk_add_f32 v[62:63], v[76:77], v[64:65]
	v_pk_add_f32 v[64:65], v[76:77], v[64:65] neg_lo:[0,1] neg_hi:[0,1]
	s_nop 0
	v_pk_mul_f32 v[72:73], v[10:11], v[64:65] op_sel:[0,1] op_sel_hi:[0,0] neg_lo:[1,1] neg_hi:[1,0]
	v_pk_fma_f32 v[64:65], v[10:11], v[64:65], v[72:73] op_sel_hi:[0,1,1] neg_lo:[1,0,0] neg_hi:[1,0,0]
	v_pk_add_f32 v[72:73], v[32:33], v[54:55]
	v_pk_add_f32 v[32:33], v[32:33], v[54:55] neg_lo:[0,1] neg_hi:[0,1]
	v_pk_add_f32 v[54:55], v[38:39], v[62:63]
	v_pk_add_f32 v[38:39], v[38:39], v[62:63] neg_lo:[0,1] neg_hi:[0,1]
	v_pk_add_f32 v[76:77], v[72:73], v[54:55]
	v_pk_add_f32 v[54:55], v[72:73], v[54:55] neg_lo:[0,1] neg_hi:[0,1]
	v_pk_add_f32 v[72:73], v[32:33], v[38:39] op_sel:[0,1] op_sel_hi:[1,0] neg_hi:[0,1]
	v_pk_add_f32 v[38:39], v[32:33], v[38:39] op_sel:[0,1] op_sel_hi:[1,0] neg_lo:[0,1]
	v_pk_add_f32 v[32:33], v[48:49], v[68:69]
	v_pk_add_f32 v[62:63], v[48:49], v[68:69] neg_lo:[0,1] neg_hi:[0,1]
	v_pk_add_f32 v[48:49], v[56:57], v[64:65]
	v_pk_add_f32 v[56:57], v[56:57], v[64:65] neg_lo:[0,1] neg_hi:[0,1]
	s_nop 0
	v_xor_b32_e32 v65, 0x80000000, v56
	v_mov_b32_e32 v64, v57
	v_pk_add_f32 v[56:57], v[32:33], v[48:49]
	v_pk_add_f32 v[48:49], v[32:33], v[48:49] neg_lo:[0,1] neg_hi:[0,1]
	v_pk_add_f32 v[68:69], v[62:63], v[64:65]
	v_pk_add_f32 v[32:33], v[62:63], v[64:65] neg_lo:[0,1] neg_hi:[0,1]
	v_pk_add_f32 v[64:65], v[66:67], v[52:53]
	v_pk_add_f32 v[52:53], v[52:53], v[66:67] neg_lo:[0,1] neg_hi:[0,1]
	v_pk_add_f32 v[62:63], v[58:59], v[82:83]
	v_pk_mul_f32 v[66:67], v[10:11], v[52:53] op_sel:[0,1] op_sel_hi:[0,0] neg_lo:[1,1] neg_hi:[1,0]
	v_pk_fma_f32 v[52:53], v[10:11], v[52:53], v[66:67] op_sel_hi:[0,1,1]
	v_pk_add_f32 v[66:67], v[74:75], v[60:61]
	v_pk_add_f32 v[60:61], v[74:75], v[60:61] neg_lo:[0,1] neg_hi:[0,1]
	v_pk_add_f32 v[58:59], v[58:59], v[82:83] neg_lo:[0,1] neg_hi:[0,1]
	v_xor_b32_e32 v75, 0x80000000, v60
	v_mov_b32_e32 v74, v61
	v_pk_add_f32 v[60:61], v[42:43], v[36:37]
	v_pk_add_f32 v[36:37], v[42:43], v[36:37] neg_lo:[0,1] neg_hi:[0,1]
	s_nop 0
	v_pk_mul_f32 v[42:43], v[10:11], v[36:37] op_sel:[0,1] op_sel_hi:[0,0] neg_lo:[1,1] neg_hi:[1,0]
	v_pk_fma_f32 v[36:37], v[10:11], v[36:37], v[42:43] op_sel_hi:[0,1,1] neg_lo:[1,0,0] neg_hi:[1,0,0]
	v_pk_add_f32 v[42:43], v[62:63], v[66:67]
	v_pk_add_f32 v[62:63], v[62:63], v[66:67] neg_lo:[0,1] neg_hi:[0,1]
	v_pk_add_f32 v[66:67], v[64:65], v[60:61]
	v_pk_add_f32 v[60:61], v[64:65], v[60:61] neg_lo:[0,1] neg_hi:[0,1]
	v_lshl_add_u32 v10, v13, 3, 0
	v_xor_b32_e32 v65, 0x80000000, v60
	v_mov_b32_e32 v64, v61
	v_pk_add_f32 v[60:61], v[42:43], v[66:67]
	v_pk_add_f32 v[66:67], v[42:43], v[66:67] neg_lo:[0,1] neg_hi:[0,1]
	v_pk_add_f32 v[82:83], v[62:63], v[64:65]
	v_pk_add_f32 v[42:43], v[62:63], v[64:65] neg_lo:[0,1] neg_hi:[0,1]
	v_pk_add_f32 v[64:65], v[52:53], v[36:37]
	v_pk_add_f32 v[36:37], v[52:53], v[36:37] neg_lo:[0,1] neg_hi:[0,1]
	v_pk_add_f32 v[62:63], v[58:59], v[74:75]
	v_pk_add_f32 v[58:59], v[58:59], v[74:75] neg_lo:[0,1] neg_hi:[0,1]
	v_pk_add_f32 v[86:87], v[62:63], v[64:65]
	v_pk_add_f32 v[52:53], v[62:63], v[64:65] neg_lo:[0,1] neg_hi:[0,1]
	v_pk_add_f32 v[62:63], v[58:59], v[36:37] op_sel:[0,1] op_sel_hi:[1,0] neg_hi:[0,1]
	v_pk_add_f32 v[36:37], v[58:59], v[36:37] op_sel:[0,1] op_sel_hi:[1,0] neg_lo:[0,1]
	v_pk_mul_f32 v[58:59], v[84:85], s[14:15] op_sel:[1,0] neg_lo:[1,0]
	s_nop 0
	v_pk_fma_f32 v[58:59], v[84:85], s[42:43], v[58:59] op_sel_hi:[0,1,1]
	ds_write_b64 v10, v[58:59]
	v_pk_fma_f32 v[58:59], v[180:181], s[92:93], v[180:181] op_sel:[1,0,0] op_sel_hi:[0,1,1]
	v_pk_mul_f32 v[64:65], v[58:59], v[76:77] op_sel:[1,1] op_sel_hi:[0,1] neg_lo:[0,1]
	v_pk_fma_f32 v[64:65], v[58:59], v[76:77], v[64:65] op_sel_hi:[1,0,1]
	ds_write_b64 v10, v[64:65] offset:4224
	v_pk_mul_f32 v[64:65], v[180:181], v[58:59] op_sel:[1,1] op_sel_hi:[0,1] neg_lo:[0,1]
	v_pk_fma_f32 v[58:59], v[180:181], v[58:59], v[64:65] op_sel_hi:[1,0,1]
	s_nop 0
	v_pk_mul_f32 v[64:65], v[58:59], v[80:81] op_sel:[1,1] op_sel_hi:[0,1] neg_lo:[0,1]
	v_pk_fma_f32 v[64:65], v[58:59], v[80:81], v[64:65] op_sel_hi:[1,0,1]
	ds_write_b64 v10, v[64:65] offset:8448
	v_pk_mul_f32 v[64:65], v[180:181], v[58:59] op_sel:[1,1] op_sel_hi:[0,1] neg_lo:[0,1]
	v_pk_fma_f32 v[58:59], v[180:181], v[58:59], v[64:65] op_sel_hi:[1,0,1]
	s_nop 0
	v_pk_mul_f32 v[64:65], v[58:59], v[60:61] op_sel:[1,1] op_sel_hi:[0,1] neg_lo:[0,1]
	v_pk_fma_f32 v[60:61], v[58:59], v[60:61], v[64:65] op_sel_hi:[1,0,1]
	ds_write_b64 v10, v[60:61] offset:12672
	v_pk_mul_f32 v[60:61], v[180:181], v[58:59] op_sel:[1,1] op_sel_hi:[0,1] neg_lo:[0,1]
	v_pk_fma_f32 v[58:59], v[180:181], v[58:59], v[60:61] op_sel_hi:[1,0,1]
	s_nop 0
	v_pk_mul_f32 v[60:61], v[70:71], v[58:59] op_sel:[1,1] op_sel_hi:[1,0] neg_lo:[1,0]
	s_nop 0
	v_pk_fma_f32 v[60:61], v[70:71], v[58:59], v[60:61] op_sel_hi:[0,1,1]
	ds_write_b64 v10, v[60:61] offset:16896
	v_pk_mul_f32 v[60:61], v[180:181], v[58:59] op_sel:[1,1] op_sel_hi:[0,1] neg_lo:[0,1]
	v_pk_fma_f32 v[58:59], v[180:181], v[58:59], v[60:61] op_sel_hi:[1,0,1]
	s_nop 0
	v_pk_mul_f32 v[60:61], v[58:59], v[56:57] op_sel:[1,1] op_sel_hi:[0,1] neg_lo:[0,1]
	v_pk_fma_f32 v[56:57], v[58:59], v[56:57], v[60:61] op_sel_hi:[1,0,1]
	ds_write_b64 v10, v[56:57] offset:21120
	v_pk_mul_f32 v[56:57], v[180:181], v[58:59] op_sel:[1,1] op_sel_hi:[0,1] neg_lo:[0,1]
	v_pk_fma_f32 v[56:57], v[180:181], v[58:59], v[56:57] op_sel_hi:[1,0,1]
	s_nop 0
	v_pk_mul_f32 v[58:59], v[78:79], v[56:57] op_sel:[1,1] op_sel_hi:[1,0] neg_lo:[1,0]
	s_nop 0
	v_pk_fma_f32 v[58:59], v[78:79], v[56:57], v[58:59] op_sel_hi:[0,1,1]
	ds_write_b64 v10, v[58:59] offset:25344
	v_pk_mul_f32 v[58:59], v[180:181], v[56:57] op_sel:[1,1] op_sel_hi:[0,1] neg_lo:[0,1]
	v_pk_fma_f32 v[56:57], v[180:181], v[56:57], v[58:59] op_sel_hi:[1,0,1]
	s_nop 0
	v_pk_mul_f32 v[58:59], v[86:87], v[56:57] op_sel:[1,1] op_sel_hi:[1,0] neg_lo:[1,0]
	s_nop 0
	v_pk_fma_f32 v[58:59], v[86:87], v[56:57], v[58:59] op_sel_hi:[0,1,1]
	ds_write_b64 v10, v[58:59] offset:29568
	v_pk_mul_f32 v[58:59], v[180:181], v[56:57] op_sel:[1,1] op_sel_hi:[0,1] neg_lo:[0,1]
	v_pk_fma_f32 v[56:57], v[180:181], v[56:57], v[58:59] op_sel_hi:[1,0,1]
	s_nop 0
	v_pk_mul_f32 v[58:59], v[46:47], v[56:57] op_sel:[1,1] op_sel_hi:[1,0] neg_lo:[1,0]
	s_nop 0
	v_pk_fma_f32 v[46:47], v[46:47], v[56:57], v[58:59] op_sel_hi:[0,1,1]
	ds_write_b64 v10, v[46:47] offset:33792
	v_pk_mul_f32 v[46:47], v[180:181], v[56:57] op_sel:[1,1] op_sel_hi:[0,1] neg_lo:[0,1]
	v_pk_fma_f32 v[46:47], v[180:181], v[56:57], v[46:47] op_sel_hi:[1,0,1]
	s_nop 0
	v_pk_mul_f32 v[56:57], v[72:73], v[46:47] op_sel:[1,1] op_sel_hi:[1,0] neg_lo:[1,0]
	s_nop 0
	v_pk_fma_f32 v[56:57], v[72:73], v[46:47], v[56:57] op_sel_hi:[0,1,1]
	ds_write_b64 v10, v[56:57] offset:38016
	v_pk_mul_f32 v[56:57], v[180:181], v[46:47] op_sel:[1,1] op_sel_hi:[0,1] neg_lo:[0,1]
	v_pk_fma_f32 v[46:47], v[180:181], v[46:47], v[56:57] op_sel_hi:[1,0,1]
	s_nop 0
	v_pk_mul_f32 v[56:57], v[50:51], v[46:47] op_sel:[1,1] op_sel_hi:[1,0] neg_lo:[1,0]
	s_nop 0
	v_pk_fma_f32 v[50:51], v[50:51], v[46:47], v[56:57] op_sel_hi:[0,1,1]
	ds_write_b64 v10, v[50:51] offset:42240
	v_pk_mul_f32 v[50:51], v[180:181], v[46:47] op_sel:[1,1] op_sel_hi:[0,1] neg_lo:[0,1]
	v_pk_fma_f32 v[46:47], v[180:181], v[46:47], v[50:51] op_sel_hi:[1,0,1]
	s_nop 0
	v_pk_mul_f32 v[50:51], v[82:83], v[46:47] op_sel:[1,1] op_sel_hi:[1,0] neg_lo:[1,0]
	s_nop 0
	v_pk_fma_f32 v[50:51], v[82:83], v[46:47], v[50:51] op_sel_hi:[0,1,1]
	ds_write_b64 v10, v[50:51] offset:46464
	v_pk_mul_f32 v[50:51], v[180:181], v[46:47] op_sel:[1,1] op_sel_hi:[0,1] neg_lo:[0,1]
	v_pk_fma_f32 v[46:47], v[180:181], v[46:47], v[50:51] op_sel_hi:[1,0,1]
	s_nop 0
	v_pk_mul_f32 v[50:51], v[40:41], v[46:47] op_sel:[1,1] op_sel_hi:[1,0] neg_lo:[1,0]
	s_nop 0
	v_pk_fma_f32 v[40:41], v[40:41], v[46:47], v[50:51] op_sel_hi:[0,1,1]
	ds_write_b64 v10, v[40:41] offset:50688
	v_pk_mul_f32 v[40:41], v[180:181], v[46:47] op_sel:[1,1] op_sel_hi:[0,1] neg_lo:[0,1]
	v_pk_fma_f32 v[40:41], v[180:181], v[46:47], v[40:41] op_sel_hi:[1,0,1]
	s_nop 0
	v_pk_mul_f32 v[46:47], v[68:69], v[40:41] op_sel:[1,1] op_sel_hi:[1,0] neg_lo:[1,0]
	s_nop 0
	v_pk_fma_f32 v[46:47], v[68:69], v[40:41], v[46:47] op_sel_hi:[0,1,1]
	ds_write_b64 v10, v[46:47] offset:54912
	v_pk_mul_f32 v[46:47], v[180:181], v[40:41] op_sel:[1,1] op_sel_hi:[0,1] neg_lo:[0,1]
	v_pk_fma_f32 v[40:41], v[180:181], v[40:41], v[46:47] op_sel_hi:[1,0,1]
	s_nop 0
	v_pk_mul_f32 v[46:47], v[44:45], v[40:41] op_sel:[1,1] op_sel_hi:[1,0] neg_lo:[1,0]
	s_nop 0
	v_pk_fma_f32 v[44:45], v[44:45], v[40:41], v[46:47] op_sel_hi:[0,1,1]
	ds_write_b64 v10, v[44:45] offset:59136
	v_pk_mul_f32 v[44:45], v[180:181], v[40:41] op_sel:[1,1] op_sel_hi:[0,1] neg_lo:[0,1]
	v_pk_fma_f32 v[40:41], v[180:181], v[40:41], v[44:45] op_sel_hi:[1,0,1]
	s_nop 0
	v_pk_mul_f32 v[44:45], v[62:63], v[40:41] op_sel:[1,1] op_sel_hi:[1,0] neg_lo:[1,0]
	s_nop 0
	v_pk_fma_f32 v[44:45], v[62:63], v[40:41], v[44:45] op_sel_hi:[0,1,1]
	ds_write_b64 v10, v[44:45] offset:63360
	v_pk_mul_f32 v[44:45], v[180:181], v[40:41] op_sel:[1,1] op_sel_hi:[0,1] neg_lo:[0,1]
	v_pk_fma_f32 v[40:41], v[180:181], v[40:41], v[44:45] op_sel_hi:[1,0,1]
	s_nop 0
	v_pk_mul_f32 v[44:45], v[30:31], v[40:41] op_sel:[1,1] op_sel_hi:[1,0] neg_lo:[1,0]
	v_add_u32_e32 v13, 0x10800, v10
	v_pk_fma_f32 v[30:31], v[30:31], v[40:41], v[44:45] op_sel_hi:[0,1,1]
	ds_write_b64 v13, v[30:31]
	v_pk_mul_f32 v[30:31], v[180:181], v[40:41] op_sel:[1,1] op_sel_hi:[0,1] neg_lo:[0,1]
	v_pk_fma_f32 v[30:31], v[180:181], v[40:41], v[30:31] op_sel_hi:[1,0,1]
	s_nop 0
	v_pk_mul_f32 v[40:41], v[54:55], v[30:31] op_sel:[1,1] op_sel_hi:[1,0] neg_lo:[1,0]
	v_add_u32_e32 v13, 0x11880, v10
	v_pk_fma_f32 v[40:41], v[54:55], v[30:31], v[40:41] op_sel_hi:[0,1,1]
	ds_write_b64 v13, v[40:41]
	v_pk_mul_f32 v[40:41], v[180:181], v[30:31] op_sel:[1,1] op_sel_hi:[0,1] neg_lo:[0,1]
	v_pk_fma_f32 v[30:31], v[180:181], v[30:31], v[40:41] op_sel_hi:[1,0,1]
	s_nop 0
	v_pk_mul_f32 v[40:41], v[34:35], v[30:31] op_sel:[1,1] op_sel_hi:[1,0] neg_lo:[1,0]
	v_add_u32_e32 v13, 0x12900, v10
	v_pk_fma_f32 v[34:35], v[34:35], v[30:31], v[40:41] op_sel_hi:[0,1,1]
	ds_write_b64 v13, v[34:35]
	v_pk_mul_f32 v[34:35], v[180:181], v[30:31] op_sel:[1,1] op_sel_hi:[0,1] neg_lo:[0,1]
	v_pk_fma_f32 v[30:31], v[180:181], v[30:31], v[34:35] op_sel_hi:[1,0,1]
	s_nop 0
	v_pk_mul_f32 v[34:35], v[66:67], v[30:31] op_sel:[1,1] op_sel_hi:[1,0] neg_lo:[1,0]
	v_add_u32_e32 v13, 0x13980, v10
	v_pk_fma_f32 v[34:35], v[66:67], v[30:31], v[34:35] op_sel_hi:[0,1,1]
	ds_write_b64 v13, v[34:35]
	v_pk_mul_f32 v[34:35], v[180:181], v[30:31] op_sel:[1,1] op_sel_hi:[0,1] neg_lo:[0,1]
	v_pk_fma_f32 v[30:31], v[180:181], v[30:31], v[34:35] op_sel_hi:[1,0,1]
	s_nop 0
	v_pk_mul_f32 v[34:35], v[26:27], v[30:31] op_sel:[1,1] op_sel_hi:[1,0] neg_lo:[1,0]
	v_add_u32_e32 v13, 0x14a00, v10
	v_pk_fma_f32 v[26:27], v[26:27], v[30:31], v[34:35] op_sel_hi:[0,1,1]
	ds_write_b64 v13, v[26:27]
	v_pk_mul_f32 v[26:27], v[180:181], v[30:31] op_sel:[1,1] op_sel_hi:[0,1] neg_lo:[0,1]
	v_pk_fma_f32 v[26:27], v[180:181], v[30:31], v[26:27] op_sel_hi:[1,0,1]
	s_nop 0
	v_pk_mul_f32 v[30:31], v[48:49], v[26:27] op_sel:[1,1] op_sel_hi:[1,0] neg_lo:[1,0]
	v_add_u32_e32 v13, 0x15a80, v10
	v_pk_fma_f32 v[30:31], v[48:49], v[26:27], v[30:31] op_sel_hi:[0,1,1]
	ds_write_b64 v13, v[30:31]
	v_pk_mul_f32 v[30:31], v[180:181], v[26:27] op_sel:[1,1] op_sel_hi:[0,1] neg_lo:[0,1]
	v_pk_fma_f32 v[26:27], v[180:181], v[26:27], v[30:31] op_sel_hi:[1,0,1]
	s_nop 0
	v_pk_mul_f32 v[30:31], v[28:29], v[26:27] op_sel:[1,1] op_sel_hi:[1,0] neg_lo:[1,0]
	v_add_u32_e32 v13, 0x16b00, v10
	v_pk_fma_f32 v[28:29], v[28:29], v[26:27], v[30:31] op_sel_hi:[0,1,1]
	ds_write_b64 v13, v[28:29]
	v_pk_mul_f32 v[28:29], v[180:181], v[26:27] op_sel:[1,1] op_sel_hi:[0,1] neg_lo:[0,1]
	v_pk_fma_f32 v[26:27], v[180:181], v[26:27], v[28:29] op_sel_hi:[1,0,1]
	s_nop 0
	v_pk_mul_f32 v[28:29], v[52:53], v[26:27] op_sel:[1,1] op_sel_hi:[1,0] neg_lo:[1,0]
	v_add_u32_e32 v13, 0x17b80, v10
	v_pk_fma_f32 v[28:29], v[52:53], v[26:27], v[28:29] op_sel_hi:[0,1,1]
	ds_write_b64 v13, v[28:29]
	v_pk_mul_f32 v[28:29], v[180:181], v[26:27] op_sel:[1,1] op_sel_hi:[0,1] neg_lo:[0,1]
	v_pk_fma_f32 v[26:27], v[180:181], v[26:27], v[28:29] op_sel_hi:[1,0,1]
	s_nop 0
	v_pk_mul_f32 v[28:29], v[22:23], v[26:27] op_sel:[1,1] op_sel_hi:[1,0] neg_lo:[1,0]
	v_add_u32_e32 v13, 0x18c00, v10
	v_pk_fma_f32 v[22:23], v[22:23], v[26:27], v[28:29] op_sel_hi:[0,1,1]
	ds_write_b64 v13, v[22:23]
	v_pk_mul_f32 v[22:23], v[180:181], v[26:27] op_sel:[1,1] op_sel_hi:[0,1] neg_lo:[0,1]
	v_pk_fma_f32 v[22:23], v[180:181], v[26:27], v[22:23] op_sel_hi:[1,0,1]
	s_nop 0
	v_pk_mul_f32 v[26:27], v[38:39], v[22:23] op_sel:[1,1] op_sel_hi:[1,0] neg_lo:[1,0]
	v_add_u32_e32 v13, 0x19c80, v10
	v_pk_fma_f32 v[26:27], v[38:39], v[22:23], v[26:27] op_sel_hi:[0,1,1]
	ds_write_b64 v13, v[26:27]
	v_pk_mul_f32 v[26:27], v[180:181], v[22:23] op_sel:[1,1] op_sel_hi:[0,1] neg_lo:[0,1]
	v_pk_fma_f32 v[22:23], v[180:181], v[22:23], v[26:27] op_sel_hi:[1,0,1]
	s_nop 0
	v_pk_mul_f32 v[26:27], v[24:25], v[22:23] op_sel:[1,1] op_sel_hi:[1,0] neg_lo:[1,0]
	v_add_u32_e32 v13, 0x1ad00, v10
	v_pk_fma_f32 v[24:25], v[24:25], v[22:23], v[26:27] op_sel_hi:[0,1,1]
	ds_write_b64 v13, v[24:25]
	v_pk_mul_f32 v[24:25], v[180:181], v[22:23] op_sel:[1,1] op_sel_hi:[0,1] neg_lo:[0,1]
	v_pk_fma_f32 v[22:23], v[180:181], v[22:23], v[24:25] op_sel_hi:[1,0,1]
	s_nop 0
	v_pk_mul_f32 v[24:25], v[42:43], v[22:23] op_sel:[1,1] op_sel_hi:[1,0] neg_lo:[1,0]
	v_add_u32_e32 v13, 0x1bd80, v10
	v_pk_fma_f32 v[24:25], v[42:43], v[22:23], v[24:25] op_sel_hi:[0,1,1]
	ds_write_b64 v13, v[24:25]
	v_pk_mul_f32 v[24:25], v[180:181], v[22:23] op_sel:[1,1] op_sel_hi:[0,1] neg_lo:[0,1]
	v_pk_fma_f32 v[22:23], v[180:181], v[22:23], v[24:25] op_sel_hi:[1,0,1]
	s_nop 0
	v_pk_mul_f32 v[24:25], v[18:19], v[22:23] op_sel:[1,1] op_sel_hi:[1,0] neg_lo:[1,0]
	v_add_u32_e32 v13, 0x1ce00, v10
	v_pk_fma_f32 v[18:19], v[18:19], v[22:23], v[24:25] op_sel_hi:[0,1,1]
	ds_write_b64 v13, v[18:19]
	v_pk_mul_f32 v[18:19], v[180:181], v[22:23] op_sel:[1,1] op_sel_hi:[0,1] neg_lo:[0,1]
	v_pk_fma_f32 v[18:19], v[180:181], v[22:23], v[18:19] op_sel_hi:[1,0,1]
	s_nop 0
	v_pk_mul_f32 v[22:23], v[32:33], v[18:19] op_sel:[1,1] op_sel_hi:[1,0] neg_lo:[1,0]
	v_add_u32_e32 v13, 0x1de80, v10
	v_pk_fma_f32 v[22:23], v[32:33], v[18:19], v[22:23] op_sel_hi:[0,1,1]
	ds_write_b64 v13, v[22:23]
	v_pk_mul_f32 v[22:23], v[180:181], v[18:19] op_sel:[1,1] op_sel_hi:[0,1] neg_lo:[0,1]
	v_pk_fma_f32 v[18:19], v[180:181], v[18:19], v[22:23] op_sel_hi:[1,0,1]
	s_nop 0
	v_pk_mul_f32 v[22:23], v[20:21], v[18:19] op_sel:[1,1] op_sel_hi:[1,0] neg_lo:[1,0]
	v_add_u32_e32 v13, 0x1ef00, v10
	v_pk_fma_f32 v[20:21], v[20:21], v[18:19], v[22:23] op_sel_hi:[0,1,1]
	ds_write_b64 v13, v[20:21]
	v_pk_mul_f32 v[20:21], v[180:181], v[18:19] op_sel:[1,1] op_sel_hi:[0,1] neg_lo:[0,1]
	v_pk_fma_f32 v[16:17], v[180:181], v[18:19], v[20:21] op_sel_hi:[1,0,1]
	s_nop 0
	v_pk_mul_f32 v[18:19], v[36:37], v[16:17] op_sel:[1,1] op_sel_hi:[1,0] neg_lo:[1,0]
	v_add_u32_e32 v10, 0x1ff80, v10
	v_pk_fma_f32 v[16:17], v[36:37], v[16:17], v[18:19] op_sel_hi:[0,1,1]
	ds_write_b64 v10, v[16:17]
	v_mov_b32_e32 v10, v176
	v_mov_b32_e32 v13, v173
	s_waitcnt lgkmcnt(0)
	s_barrier
	v_mov_b32_e32 v16, v182
	v_add_u32_e32 v15, v13, v10
	v_lshl_add_u32 v75, v15, 3, 0
	v_xad_u32 v15, v13, 1, v10
	v_lshl_add_u32 v74, v15, 3, 0
	v_xad_u32 v15, v13, 2, v10
	v_lshl_add_u32 v73, v15, 3, 0
	v_xad_u32 v15, v13, 3, v10
	v_lshl_add_u32 v72, v15, 3, 0
	v_xad_u32 v15, v13, 4, v10
	v_lshl_add_u32 v71, v15, 3, 0
	v_xad_u32 v15, v13, 5, v10
	v_lshl_add_u32 v70, v15, 3, 0
	v_xad_u32 v15, v13, 6, v10
	v_lshl_add_u32 v69, v15, 3, 0
	v_xad_u32 v15, v13, 7, v10
	v_lshl_add_u32 v68, v15, 3, 0
	v_xad_u32 v15, v13, 8, v10
	v_lshl_add_u32 v15, v15, 3, 0
	v_add_u32_e32 v67, 0x800, v15
	v_xad_u32 v15, v13, 9, v10
	v_lshl_add_u32 v15, v15, 3, 0
	v_add_u32_e32 v66, 0x800, v15
	v_xad_u32 v15, v13, 10, v10
	v_lshl_add_u32 v15, v15, 3, 0
	v_add_u32_e32 v65, 0x800, v15
	v_xad_u32 v15, v13, 11, v10
	v_lshl_add_u32 v15, v15, 3, 0
	v_add_u32_e32 v64, 0x800, v15
	v_xad_u32 v15, v13, 12, v10
	v_mov_b32_e32 v17, v183
	v_lshl_add_u32 v15, v15, 3, 0
	ds_read2_b64 v[18:21], v75 offset1:16
	ds_read2_b64 v[40:43], v67 offset1:16
	v_add_u32_e32 v63, 0x800, v15
	v_xad_u32 v15, v13, 13, v10
	v_lshl_add_u32 v15, v15, 3, 0
	v_add_u32_e32 v62, 0x800, v15
	v_xad_u32 v15, v13, 14, v10
	v_xad_u32 v10, v13, 15, v10
	ds_read2_b64 v[22:25], v74 offset0:32 offset1:48
	ds_read2_b64 v[48:51], v66 offset0:32 offset1:48
	v_lshl_add_u32 v15, v15, 3, 0
	v_lshl_add_u32 v10, v10, 3, 0
	v_add_u32_e32 v15, 0x800, v15
	v_add_u32_e32 v13, 0x800, v10
	v_mov_b32_e32 v10, v164
	ds_read2_b64 v[26:29], v73 offset0:64 offset1:80
	ds_read2_b64 v[58:61], v72 offset0:96 offset1:112
	ds_read2_b64 v[76:79], v71 offset0:128 offset1:144
	ds_read2_b64 v[80:83], v70 offset0:160 offset1:176
	ds_read2_b64 v[84:87], v69 offset0:192 offset1:208
	ds_read2_b64 v[88:91], v68 offset0:224 offset1:240
	ds_read2_b64 v[54:57], v65 offset0:64 offset1:80
	ds_read2_b64 v[92:95], v64 offset0:96 offset1:112
	ds_read2_b64 v[96:99], v63 offset0:128 offset1:144
	ds_read2_b64 v[100:103], v62 offset0:160 offset1:176
	ds_read2_b64 v[104:107], v15 offset0:192 offset1:208
	ds_read2_b64 v[108:111], v13 offset0:224 offset1:240
	s_waitcnt lgkmcnt(14)
	v_pk_add_f32 v[112:113], v[18:19], v[40:41]
	v_pk_add_f32 v[40:41], v[18:19], v[40:41] neg_lo:[0,1] neg_hi:[0,1]
	v_pk_add_f32 v[18:19], v[20:21], v[42:43]
	v_pk_add_f32 v[20:21], v[20:21], v[42:43] neg_lo:[0,1] neg_hi:[0,1]
	v_mov_b32_e32 v30, v165
	v_mov_b32_e32 v32, v166
	v_mov_b32_e32 v34, v167
	v_mov_b32_e32 v10, v168
	v_mov_b32_e32 v38, v169
	v_mov_b32_e32 v36, v170
	v_mov_b32_e32 v46, v171
	v_mov_b32_e32 v31, v172
	v_pk_mul_f32 v[42:43], v[20:21], v[46:47] op_sel:[1,0] op_sel_hi:[0,0] neg_lo:[1,1] neg_hi:[0,1]
	s_nop 0
	v_pk_fma_f32 v[44:45], v[20:21], v[30:31], v[42:43] op_sel_hi:[1,0,1]
	s_waitcnt lgkmcnt(12)
	v_pk_add_f32 v[20:21], v[22:23], v[48:49]
	v_pk_add_f32 v[22:23], v[22:23], v[48:49] neg_lo:[0,1] neg_hi:[0,1]
	s_nop 0
	v_pk_mul_f32 v[42:43], v[22:23], v[36:37] op_sel:[1,0] op_sel_hi:[0,0] neg_lo:[1,1] neg_hi:[0,1]
	s_nop 0
	v_pk_fma_f32 v[48:49], v[22:23], v[32:33], v[42:43] op_sel_hi:[1,0,1]
	v_pk_add_f32 v[22:23], v[24:25], v[50:51]
	v_pk_add_f32 v[24:25], v[24:25], v[50:51] neg_lo:[0,1] neg_hi:[0,1]
	s_nop 0
	v_pk_mul_f32 v[42:43], v[24:25], v[38:39] op_sel:[1,0] op_sel_hi:[0,0] neg_lo:[1,1] neg_hi:[0,1]
	s_nop 0
	v_pk_fma_f32 v[52:53], v[24:25], v[34:35], v[42:43] op_sel_hi:[1,0,1]
	s_waitcnt lgkmcnt(5)
	v_pk_add_f32 v[24:25], v[26:27], v[54:55]
	v_pk_add_f32 v[26:27], v[26:27], v[54:55] neg_lo:[0,1] neg_hi:[0,1]
	s_nop 0
	v_pk_mul_f32 v[42:43], v[26:27], v[10:11] op_sel:[1,0] op_sel_hi:[0,0] neg_lo:[1,1] neg_hi:[0,1]
	s_nop 0
	v_pk_fma_f32 v[54:55], v[26:27], v[10:11], v[42:43] op_sel_hi:[1,0,1]
	v_pk_add_f32 v[26:27], v[28:29], v[56:57]
	v_pk_add_f32 v[28:29], v[28:29], v[56:57] neg_lo:[0,1] neg_hi:[0,1]
	s_nop 0
	v_pk_mul_f32 v[42:43], v[28:29], v[38:39] op_sel_hi:[1,0]
	s_nop 0
	v_pk_fma_f32 v[56:57], v[28:29], v[34:35], v[42:43] op_sel:[1,0,0] op_sel_hi:[0,0,1] neg_lo:[1,1,0] neg_hi:[0,1,0]
	s_waitcnt lgkmcnt(4)
	v_pk_add_f32 v[42:43], v[58:59], v[92:93] neg_lo:[0,1] neg_hi:[0,1]
	v_pk_add_f32 v[28:29], v[58:59], v[92:93]
	v_pk_mul_f32 v[50:51], v[42:43], v[36:37] op_sel_hi:[1,0]
	s_nop 0
	v_pk_fma_f32 v[58:59], v[42:43], v[32:33], v[50:51] op_sel:[1,0,0] op_sel_hi:[0,0,1] neg_lo:[1,1,0] neg_hi:[0,1,0]
	v_pk_add_f32 v[50:51], v[60:61], v[94:95] neg_lo:[0,1] neg_hi:[0,1]
	v_pk_add_f32 v[42:43], v[60:61], v[94:95]
	v_pk_mul_f32 v[60:61], v[50:51], v[46:47] op_sel_hi:[1,0]
	v_xor_b32_e32 v92, 0x80000000, v51
	v_mov_b32_e32 v93, v50
	s_waitcnt lgkmcnt(3)
	v_pk_add_f32 v[50:51], v[76:77], v[96:97]
	v_pk_add_f32 v[76:77], v[76:77], v[96:97] neg_lo:[0,1] neg_hi:[0,1]
	v_pk_fma_f32 v[60:61], v[92:93], v[30:31], v[60:61] op_sel_hi:[1,0,1] neg_lo:[0,1,0] neg_hi:[0,1,0]
	v_xor_b32_e32 v93, 0x80000000, v76
	v_mov_b32_e32 v92, v77
	v_pk_add_f32 v[76:77], v[78:79], v[98:99]
	v_pk_add_f32 v[78:79], v[78:79], v[98:99] neg_lo:[0,1] neg_hi:[0,1]
	s_nop 0
	v_pk_mul_f32 v[94:95], v[78:79], v[46:47] op_sel_hi:[1,0] neg_lo:[0,1] neg_hi:[0,1]
	s_nop 0
	v_pk_fma_f32 v[78:79], v[78:79], v[30:31], v[94:95] op_sel:[1,0,0] op_sel_hi:[0,0,1] neg_lo:[1,1,0] neg_hi:[0,1,0]
	s_waitcnt lgkmcnt(2)
	v_pk_add_f32 v[94:95], v[80:81], v[100:101]
	v_pk_add_f32 v[80:81], v[80:81], v[100:101] neg_lo:[0,1] neg_hi:[0,1]
	s_nop 0
	v_pk_mul_f32 v[96:97], v[80:81], v[36:37] op_sel_hi:[1,0] neg_lo:[0,1] neg_hi:[0,1]
	s_nop 0
	v_pk_fma_f32 v[80:81], v[80:81], v[32:33], v[96:97] op_sel:[1,0,0] op_sel_hi:[0,0,1] neg_lo:[1,1,0] neg_hi:[0,1,0]
	v_pk_add_f32 v[96:97], v[82:83], v[102:103]
	v_pk_add_f32 v[82:83], v[82:83], v[102:103] neg_lo:[0,1] neg_hi:[0,1]
	s_nop 0
	v_pk_mul_f32 v[98:99], v[82:83], v[38:39] op_sel_hi:[1,0] neg_lo:[0,1] neg_hi:[0,1]
	s_nop 0
	v_pk_fma_f32 v[82:83], v[82:83], v[34:35], v[98:99] op_sel:[1,0,0] op_sel_hi:[0,0,1] neg_lo:[1,1,0] neg_hi:[0,1,0]
	s_waitcnt lgkmcnt(1)
	v_pk_add_f32 v[98:99], v[84:85], v[104:105]
	v_pk_add_f32 v[84:85], v[84:85], v[104:105] neg_lo:[0,1] neg_hi:[0,1]
	s_nop 0
	v_pk_mul_f32 v[100:101], v[84:85], v[10:11] op_sel:[1,0] op_sel_hi:[0,0] neg_lo:[1,1] neg_hi:[0,1]
	s_nop 0
	v_pk_fma_f32 v[84:85], v[84:85], v[10:11], v[100:101] op_sel_hi:[1,0,1] neg_lo:[0,1,0] neg_hi:[0,1,0]
	v_pk_add_f32 v[100:101], v[86:87], v[106:107]
	v_pk_add_f32 v[86:87], v[86:87], v[106:107] neg_lo:[0,1] neg_hi:[0,1]
	s_nop 0
	v_pk_mul_f32 v[38:39], v[86:87], v[38:39] op_sel:[1,0] op_sel_hi:[0,0] neg_lo:[1,1] neg_hi:[0,1]
	s_nop 0
	v_pk_fma_f32 v[86:87], v[86:87], v[34:35], v[38:39] op_sel_hi:[1,0,1] neg_lo:[0,1,0] neg_hi:[0,1,0]
	s_waitcnt lgkmcnt(0)
	v_pk_add_f32 v[38:39], v[88:89], v[108:109] neg_lo:[0,1] neg_hi:[0,1]
	v_pk_add_f32 v[34:35], v[88:89], v[108:109]
	v_pk_mul_f32 v[88:89], v[38:39], v[36:37] op_sel:[1,0] op_sel_hi:[0,0] neg_lo:[1,1] neg_hi:[0,1]
	s_nop 0
	v_pk_fma_f32 v[88:89], v[38:39], v[32:33], v[88:89] op_sel_hi:[1,0,1] neg_lo:[0,1,0] neg_hi:[0,1,0]
	v_pk_add_f32 v[38:39], v[90:91], v[110:111]
	v_pk_add_f32 v[90:91], v[90:91], v[110:111] neg_lo:[0,1] neg_hi:[0,1]
	s_nop 0
	v_pk_mul_f32 v[46:47], v[90:91], v[46:47] op_sel:[1,0] op_sel_hi:[0,0] neg_lo:[1,1] neg_hi:[0,1]
	s_nop 0
	v_pk_fma_f32 v[90:91], v[90:91], v[30:31], v[46:47] op_sel_hi:[1,0,1] neg_lo:[0,1,0] neg_hi:[0,1,0]
	v_pk_add_f32 v[46:47], v[18:19], v[76:77]
	v_pk_add_f32 v[18:19], v[18:19], v[76:77] neg_lo:[0,1] neg_hi:[0,1]
	v_pk_add_f32 v[30:31], v[112:113], v[50:51]
	v_pk_mul_f32 v[76:77], v[18:19], v[36:37] op_sel:[1,0] op_sel_hi:[0,0] neg_lo:[1,1] neg_hi:[0,1]
	v_pk_add_f32 v[50:51], v[112:113], v[50:51] neg_lo:[0,1] neg_hi:[0,1]
	v_pk_fma_f32 v[76:77], v[18:19], v[32:33], v[76:77] op_sel_hi:[1,0,1]
	v_pk_add_f32 v[18:19], v[20:21], v[94:95]
	v_pk_add_f32 v[20:21], v[20:21], v[94:95] neg_lo:[0,1] neg_hi:[0,1]
	s_nop 0
	v_pk_mul_f32 v[94:95], v[20:21], v[10:11] op_sel:[1,0] op_sel_hi:[0,0] neg_lo:[1,1] neg_hi:[0,1]
	s_nop 0
	v_pk_fma_f32 v[20:21], v[20:21], v[10:11], v[94:95] op_sel_hi:[1,0,1]
	v_pk_add_f32 v[94:95], v[22:23], v[96:97]
	v_pk_add_f32 v[22:23], v[22:23], v[96:97] neg_lo:[0,1] neg_hi:[0,1]
	s_nop 0
	v_pk_mul_f32 v[96:97], v[22:23], v[36:37] op_sel_hi:[1,0]
	v_xor_b32_e32 v102, 0x80000000, v23
	v_mov_b32_e32 v103, v22
	v_pk_add_f32 v[22:23], v[24:25], v[98:99]
	v_pk_add_f32 v[24:25], v[24:25], v[98:99] neg_lo:[0,1] neg_hi:[0,1]
	v_pk_fma_f32 v[96:97], v[102:103], v[32:33], v[96:97] op_sel_hi:[1,0,1] neg_lo:[0,1,0] neg_hi:[0,1,0]
	v_xor_b32_e32 v99, 0x80000000, v24
	v_mov_b32_e32 v98, v25
	v_pk_add_f32 v[24:25], v[26:27], v[100:101]
	v_pk_add_f32 v[26:27], v[26:27], v[100:101] neg_lo:[0,1] neg_hi:[0,1]
	s_nop 0
	v_pk_mul_f32 v[100:101], v[26:27], v[36:37] op_sel_hi:[1,0] neg_lo:[0,1] neg_hi:[0,1]
	v_xor_b32_e32 v102, 0x80000000, v27
	v_mov_b32_e32 v103, v26
	v_pk_add_f32 v[26:27], v[28:29], v[34:35]
	v_pk_add_f32 v[28:29], v[28:29], v[34:35] neg_lo:[0,1] neg_hi:[0,1]
	v_pk_fma_f32 v[100:101], v[102:103], v[32:33], v[100:101] op_sel_hi:[1,0,1] neg_lo:[0,1,0] neg_hi:[0,1,0]
	v_pk_mul_f32 v[34:35], v[28:29], v[10:11] op_sel:[1,0] op_sel_hi:[0,0] neg_lo:[1,1] neg_hi:[0,1]
	v_pk_add_f32 v[102:103], v[30:31], v[22:23] neg_lo:[0,1] neg_hi:[0,1]
	v_pk_fma_f32 v[28:29], v[28:29], v[10:11], v[34:35] op_sel_hi:[1,0,1] neg_lo:[0,1,0] neg_hi:[0,1,0]
	v_pk_add_f32 v[34:35], v[42:43], v[38:39]
	v_pk_add_f32 v[38:39], v[42:43], v[38:39] neg_lo:[0,1] neg_hi:[0,1]
	s_nop 0
	v_pk_mul_f32 v[42:43], v[38:39], v[36:37] op_sel:[1,0] op_sel_hi:[0,0] neg_lo:[1,1] neg_hi:[0,1]
	s_nop 0
	v_pk_fma_f32 v[42:43], v[38:39], v[32:33], v[42:43] op_sel_hi:[1,0,1] neg_lo:[0,1,0] neg_hi:[0,1,0]
	v_pk_add_f32 v[38:39], v[30:31], v[22:23]
	v_pk_add_f32 v[22:23], v[46:47], v[24:25]
	v_pk_add_f32 v[24:25], v[46:47], v[24:25] neg_lo:[0,1] neg_hi:[0,1]
	s_nop 0
	v_pk_mul_f32 v[30:31], v[24:25], v[10:11] op_sel:[1,0] op_sel_hi:[0,0] neg_lo:[1,1] neg_hi:[0,1]
	s_nop 0
	v_pk_fma_f32 v[24:25], v[24:25], v[10:11], v[30:31] op_sel_hi:[1,0,1]
	v_pk_add_f32 v[30:31], v[18:19], v[26:27]
	v_pk_add_f32 v[18:19], v[18:19], v[26:27] neg_lo:[0,1] neg_hi:[0,1]
	s_nop 0
	v_xor_b32_e32 v27, 0x80000000, v18
	v_mov_b32_e32 v26, v19
	v_pk_add_f32 v[18:19], v[94:95], v[34:35]
	v_pk_add_f32 v[34:35], v[94:95], v[34:35] neg_lo:[0,1] neg_hi:[0,1]
	s_nop 0
	v_pk_mul_f32 v[46:47], v[34:35], v[10:11] op_sel:[1,0] op_sel_hi:[0,0] neg_lo:[1,1] neg_hi:[0,1]
	s_nop 0
	v_pk_fma_f32 v[34:35], v[34:35], v[10:11], v[46:47] op_sel_hi:[1,0,1] neg_lo:[0,1,0] neg_hi:[0,1,0]
	v_pk_add_f32 v[46:47], v[38:39], v[30:31]
	v_pk_add_f32 v[38:39], v[38:39], v[30:31] neg_lo:[0,1] neg_hi:[0,1]
	v_pk_add_f32 v[30:31], v[22:23], v[18:19]
	v_pk_add_f32 v[18:19], v[22:23], v[18:19] neg_lo:[0,1] neg_hi:[0,1]
	v_pk_add_f32 v[94:95], v[46:47], v[30:31]
	v_xor_b32_e32 v23, 0x80000000, v18
	v_mov_b32_e32 v22, v19
	v_pk_add_f32 v[18:19], v[102:103], v[26:27]
	v_pk_add_f32 v[102:103], v[102:103], v[26:27] neg_lo:[0,1] neg_hi:[0,1]
	v_pk_add_f32 v[26:27], v[24:25], v[34:35]
	v_pk_add_f32 v[24:25], v[24:25], v[34:35] neg_lo:[0,1] neg_hi:[0,1]
	v_pk_add_f32 v[30:31], v[46:47], v[30:31] neg_lo:[0,1] neg_hi:[0,1]
	v_xor_b32_e32 v35, 0x80000000, v24
	v_mov_b32_e32 v34, v25
	v_pk_add_f32 v[24:25], v[50:51], v[98:99]
	v_pk_add_f32 v[98:99], v[50:51], v[98:99] neg_lo:[0,1] neg_hi:[0,1]
	v_pk_add_f32 v[50:51], v[76:77], v[100:101] neg_lo:[0,1] neg_hi:[0,1]
	v_pk_add_f32 v[46:47], v[38:39], v[22:23]
	v_pk_add_f32 v[22:23], v[38:39], v[22:23] neg_lo:[0,1] neg_hi:[0,1]
	v_pk_add_f32 v[104:105], v[18:19], v[26:27]
	v_pk_add_f32 v[26:27], v[18:19], v[26:27] neg_lo:[0,1] neg_hi:[0,1]
	v_pk_add_f32 v[38:39], v[102:103], v[34:35]
	v_pk_add_f32 v[18:19], v[102:103], v[34:35] neg_lo:[0,1] neg_hi:[0,1]
	v_pk_add_f32 v[34:35], v[76:77], v[100:101]
	v_pk_mul_f32 v[76:77], v[10:11], v[50:51] op_sel:[0,1] op_sel_hi:[0,0] neg_lo:[1,1] neg_hi:[1,0]
	v_pk_fma_f32 v[76:77], v[10:11], v[50:51], v[76:77] op_sel_hi:[0,1,1]
	v_pk_add_f32 v[50:51], v[20:21], v[28:29]
	v_pk_add_f32 v[20:21], v[20:21], v[28:29] neg_lo:[0,1] neg_hi:[0,1]
	s_nop 0
	v_xor_b32_e32 v29, 0x80000000, v20
	v_mov_b32_e32 v28, v21
	v_pk_add_f32 v[20:21], v[96:97], v[42:43]
	v_pk_add_f32 v[42:43], v[96:97], v[42:43] neg_lo:[0,1] neg_hi:[0,1]
	s_nop 0
	v_pk_mul_f32 v[96:97], v[10:11], v[42:43] op_sel:[0,1] op_sel_hi:[0,0] neg_lo:[1,1] neg_hi:[1,0]
	v_pk_fma_f32 v[42:43], v[10:11], v[42:43], v[96:97] op_sel_hi:[0,1,1] neg_lo:[1,0,0] neg_hi:[1,0,0]
	v_pk_add_f32 v[96:97], v[24:25], v[50:51]
	v_pk_add_f32 v[24:25], v[24:25], v[50:51] neg_lo:[0,1] neg_hi:[0,1]
	v_pk_add_f32 v[50:51], v[34:35], v[20:21]
	v_pk_add_f32 v[20:21], v[34:35], v[20:21] neg_lo:[0,1] neg_hi:[0,1]
	v_pk_add_f32 v[102:103], v[96:97], v[50:51]
	v_xor_b32_e32 v101, 0x80000000, v20
	v_mov_b32_e32 v100, v21
	v_pk_add_f32 v[34:35], v[96:97], v[50:51] neg_lo:[0,1] neg_hi:[0,1]
	v_pk_add_f32 v[20:21], v[98:99], v[28:29]
	v_pk_add_f32 v[96:97], v[98:99], v[28:29] neg_lo:[0,1] neg_hi:[0,1]
	v_pk_add_f32 v[28:29], v[76:77], v[42:43]
	v_pk_add_f32 v[42:43], v[76:77], v[42:43] neg_lo:[0,1] neg_hi:[0,1]
	v_pk_add_f32 v[98:99], v[20:21], v[28:29]
	v_xor_b32_e32 v77, 0x80000000, v42
	v_mov_b32_e32 v76, v43
	v_pk_add_f32 v[28:29], v[20:21], v[28:29] neg_lo:[0,1] neg_hi:[0,1]
	v_pk_add_f32 v[42:43], v[96:97], v[76:77]
	v_pk_add_f32 v[20:21], v[96:97], v[76:77] neg_lo:[0,1] neg_hi:[0,1]
	v_pk_add_f32 v[76:77], v[40:41], v[92:93]
	v_pk_add_f32 v[92:93], v[40:41], v[92:93] neg_lo:[0,1] neg_hi:[0,1]
	v_pk_add_f32 v[40:41], v[44:45], v[78:79]
	v_pk_add_f32 v[44:45], v[44:45], v[78:79] neg_lo:[0,1] neg_hi:[0,1]
	v_pk_add_f32 v[50:51], v[24:25], v[100:101]
	v_pk_mul_f32 v[78:79], v[36:37], v[44:45] op_sel:[0,1] op_sel_hi:[0,0] neg_lo:[1,1] neg_hi:[1,0]
	v_pk_fma_f32 v[44:45], v[32:33], v[44:45], v[78:79] op_sel_hi:[0,1,1]
	v_pk_add_f32 v[78:79], v[48:49], v[80:81]
	v_pk_add_f32 v[48:49], v[48:49], v[80:81] neg_lo:[0,1] neg_hi:[0,1]
	v_pk_add_f32 v[24:25], v[24:25], v[100:101] neg_lo:[0,1] neg_hi:[0,1]
	v_pk_mul_f32 v[80:81], v[10:11], v[48:49] op_sel:[0,1] op_sel_hi:[0,0] neg_lo:[1,1] neg_hi:[1,0]
	v_pk_fma_f32 v[80:81], v[10:11], v[48:49], v[80:81] op_sel_hi:[0,1,1]
	v_pk_add_f32 v[48:49], v[52:53], v[82:83]
	v_pk_add_f32 v[52:53], v[52:53], v[82:83] neg_lo:[0,1] neg_hi:[0,1]
	s_nop 0
	v_pk_mul_f32 v[82:83], v[32:33], v[52:53] op_sel:[0,1] op_sel_hi:[0,0] neg_lo:[1,1] neg_hi:[1,0]
	v_pk_fma_f32 v[52:53], v[36:37], v[52:53], v[82:83] op_sel_hi:[0,1,1]
	v_pk_add_f32 v[82:83], v[54:55], v[84:85]
	v_pk_add_f32 v[54:55], v[54:55], v[84:85] neg_lo:[0,1] neg_hi:[0,1]
	s_nop 0
	v_xor_b32_e32 v85, 0x80000000, v54
	v_mov_b32_e32 v84, v55
	v_pk_add_f32 v[54:55], v[56:57], v[86:87]
	v_pk_add_f32 v[56:57], v[56:57], v[86:87] neg_lo:[0,1] neg_hi:[0,1]
	s_nop 0
	v_pk_mul_f32 v[86:87], v[32:33], v[56:57] op_sel:[0,1] op_sel_hi:[0,0] neg_lo:[1,1] neg_hi:[1,0]
	v_pk_fma_f32 v[56:57], v[36:37], v[56:57], v[86:87] op_sel_hi:[0,1,1] neg_lo:[1,0,0] neg_hi:[1,0,0]
	v_pk_add_f32 v[86:87], v[58:59], v[88:89]
	v_pk_add_f32 v[58:59], v[58:59], v[88:89] neg_lo:[0,1] neg_hi:[0,1]
	s_nop 0
	v_pk_mul_f32 v[88:89], v[10:11], v[58:59] op_sel:[0,1] op_sel_hi:[0,0] neg_lo:[1,1] neg_hi:[1,0]
	v_pk_fma_f32 v[58:59], v[10:11], v[58:59], v[88:89] op_sel_hi:[0,1,1] neg_lo:[1,0,0] neg_hi:[1,0,0]
	v_pk_add_f32 v[88:89], v[60:61], v[90:91]
	v_pk_add_f32 v[60:61], v[60:61], v[90:91] neg_lo:[0,1] neg_hi:[0,1]
	s_nop 0
	v_pk_mul_f32 v[36:37], v[36:37], v[60:61] op_sel:[0,1] op_sel_hi:[0,0] neg_lo:[1,1] neg_hi:[1,0]
	v_pk_fma_f32 v[36:37], v[32:33], v[60:61], v[36:37] op_sel_hi:[0,1,1] neg_lo:[1,0,0] neg_hi:[1,0,0]
	v_pk_add_f32 v[32:33], v[76:77], v[82:83]
	v_pk_add_f32 v[60:61], v[76:77], v[82:83] neg_lo:[0,1] neg_hi:[0,1]
	v_pk_add_f32 v[76:77], v[54:55], v[40:41]
	v_pk_add_f32 v[40:41], v[40:41], v[54:55] neg_lo:[0,1] neg_hi:[0,1]
	s_nop 0
	v_pk_mul_f32 v[54:55], v[10:11], v[40:41] op_sel:[0,1] op_sel_hi:[0,0] neg_lo:[1,1] neg_hi:[1,0]
	v_pk_fma_f32 v[54:55], v[10:11], v[40:41], v[54:55] op_sel_hi:[0,1,1]
	v_pk_add_f32 v[40:41], v[78:79], v[86:87]
	v_pk_add_f32 v[78:79], v[78:79], v[86:87] neg_lo:[0,1] neg_hi:[0,1]
	s_nop 0
	v_xor_b32_e32 v83, 0x80000000, v78
	v_mov_b32_e32 v82, v79
	v_pk_add_f32 v[78:79], v[48:49], v[88:89]
	v_pk_add_f32 v[48:49], v[48:49], v[88:89] neg_lo:[0,1] neg_hi:[0,1]
	v_pk_add_f32 v[88:89], v[76:77], v[78:79]
	v_pk_mul_f32 v[86:87], v[10:11], v[48:49] op_sel:[0,1] op_sel_hi:[0,0] neg_lo:[1,1] neg_hi:[1,0]
	v_pk_fma_f32 v[48:49], v[10:11], v[48:49], v[86:87] op_sel_hi:[0,1,1] neg_lo:[1,0,0] neg_hi:[1,0,0]
	v_pk_add_f32 v[86:87], v[32:33], v[40:41]
	v_pk_add_f32 v[32:33], v[32:33], v[40:41] neg_lo:[0,1] neg_hi:[0,1]
	v_pk_add_f32 v[40:41], v[76:77], v[78:79] neg_lo:[0,1] neg_hi:[0,1]
	v_pk_add_f32 v[78:79], v[86:87], v[88:89] neg_lo:[0,1] neg_hi:[0,1]
	v_pk_add_f32 v[90:91], v[32:33], v[40:41] op_sel:[0,1] op_sel_hi:[1,0] neg_hi:[0,1]
	v_pk_add_f32 v[40:41], v[32:33], v[40:41] op_sel:[0,1] op_sel_hi:[1,0] neg_lo:[0,1]
	v_pk_add_f32 v[76:77], v[54:55], v[48:49]
	v_pk_add_f32 v[48:49], v[54:55], v[48:49] neg_lo:[0,1] neg_hi:[0,1]
	v_pk_add_f32 v[32:33], v[60:61], v[82:83]
	v_pk_add_f32 v[60:61], v[60:61], v[82:83] neg_lo:[0,1] neg_hi:[0,1]
	v_xor_b32_e32 v55, 0x80000000, v48
	v_mov_b32_e32 v54, v49
	v_pk_add_f32 v[82:83], v[32:33], v[76:77]
	v_pk_add_f32 v[48:49], v[32:33], v[76:77] neg_lo:[0,1] neg_hi:[0,1]
	v_pk_add_f32 v[76:77], v[60:61], v[54:55]
	v_pk_add_f32 v[32:33], v[60:61], v[54:55] neg_lo:[0,1] neg_hi:[0,1]
	v_pk_add_f32 v[54:55], v[92:93], v[84:85]
	v_pk_add_f32 v[60:61], v[92:93], v[84:85] neg_lo:[0,1] neg_hi:[0,1]
	v_pk_add_f32 v[84:85], v[56:57], v[44:45]
	v_pk_add_f32 v[44:45], v[44:45], v[56:57] neg_lo:[0,1] neg_hi:[0,1]
	v_pk_add_f32 v[86:87], v[86:87], v[88:89]
	v_pk_mul_f32 v[56:57], v[10:11], v[44:45] op_sel:[0,1] op_sel_hi:[0,0] neg_lo:[1,1] neg_hi:[1,0]
	v_pk_fma_f32 v[56:57], v[10:11], v[44:45], v[56:57] op_sel_hi:[0,1,1]
	v_pk_add_f32 v[44:45], v[80:81], v[58:59]
	v_pk_add_f32 v[58:59], v[80:81], v[58:59] neg_lo:[0,1] neg_hi:[0,1]
	s_nop 0
	v_xor_b32_e32 v81, 0x80000000, v58
	v_mov_b32_e32 v80, v59
	v_pk_add_f32 v[58:59], v[52:53], v[36:37]
	v_pk_add_f32 v[36:37], v[52:53], v[36:37] neg_lo:[0,1] neg_hi:[0,1]
	s_nop 0
	v_pk_mul_f32 v[52:53], v[10:11], v[36:37] op_sel:[0,1] op_sel_hi:[0,0] neg_lo:[1,1] neg_hi:[1,0]
	v_pk_fma_f32 v[36:37], v[10:11], v[36:37], v[52:53] op_sel_hi:[0,1,1] neg_lo:[1,0,0] neg_hi:[1,0,0]
	v_pk_add_f32 v[52:53], v[54:55], v[44:45]
	v_pk_add_f32 v[44:45], v[54:55], v[44:45] neg_lo:[0,1] neg_hi:[0,1]
	v_pk_add_f32 v[54:55], v[84:85], v[58:59]
	v_pk_add_f32 v[58:59], v[84:85], v[58:59] neg_lo:[0,1] neg_hi:[0,1]
	s_nop 0
	v_xor_b32_e32 v85, 0x80000000, v58
	v_mov_b32_e32 v84, v59
	v_pk_add_f32 v[58:59], v[52:53], v[54:55]
	v_pk_add_f32 v[52:53], v[52:53], v[54:55] neg_lo:[0,1] neg_hi:[0,1]
	v_pk_add_f32 v[54:55], v[44:45], v[84:85]
	v_pk_add_f32 v[44:45], v[44:45], v[84:85] neg_lo:[0,1] neg_hi:[0,1]
	v_pk_add_f32 v[84:85], v[60:61], v[80:81]
	v_pk_add_f32 v[60:61], v[60:61], v[80:81] neg_lo:[0,1] neg_hi:[0,1]
	v_pk_add_f32 v[80:81], v[56:57], v[36:37]
	v_pk_add_f32 v[36:37], v[56:57], v[36:37] neg_lo:[0,1] neg_hi:[0,1]
	v_pk_add_f32 v[92:93], v[84:85], v[80:81]
	v_pk_add_f32 v[80:81], v[84:85], v[80:81] neg_lo:[0,1] neg_hi:[0,1]
	v_pk_add_f32 v[84:85], v[60:61], v[36:37] op_sel:[0,1] op_sel_hi:[1,0] neg_hi:[0,1]
	v_pk_add_f32 v[36:37], v[60:61], v[36:37] op_sel:[0,1] op_sel_hi:[1,0] neg_lo:[0,1]
	v_pk_fma_f32 v[60:61], v[16:17], s[92:93], v[16:17] op_sel:[1,0,0] op_sel_hi:[0,1,1]
	v_pk_mul_f32 v[56:57], v[94:95], s[14:15] op_sel:[1,0] neg_lo:[1,0]
	v_pk_mul_f32 v[88:89], v[60:61], v[86:87] op_sel:[1,1] op_sel_hi:[0,1] neg_lo:[0,1]
	v_pk_fma_f32 v[56:57], v[94:95], s[42:43], v[56:57] op_sel_hi:[0,1,1]
	v_pk_fma_f32 v[86:87], v[60:61], v[86:87], v[88:89] op_sel_hi:[1,0,1]
	ds_write2_b64 v75, v[56:57], v[86:87] offset1:16
	v_pk_mul_f32 v[56:57], v[16:17], v[60:61] op_sel:[1,1] op_sel_hi:[0,1] neg_lo:[0,1]
	v_pk_fma_f32 v[56:57], v[16:17], v[60:61], v[56:57] op_sel_hi:[1,0,1]
	s_nop 0
	v_pk_mul_f32 v[60:61], v[56:57], v[102:103] op_sel:[1,1] op_sel_hi:[0,1] neg_lo:[0,1]
	v_pk_mul_f32 v[86:87], v[16:17], v[56:57] op_sel:[1,1] op_sel_hi:[0,1] neg_lo:[0,1]
	v_pk_fma_f32 v[60:61], v[56:57], v[102:103], v[60:61] op_sel_hi:[1,0,1]
	v_pk_fma_f32 v[56:57], v[16:17], v[56:57], v[86:87] op_sel_hi:[1,0,1]
	s_nop 0
	v_pk_mul_f32 v[86:87], v[56:57], v[58:59] op_sel:[1,1] op_sel_hi:[0,1] neg_lo:[0,1]
	v_pk_fma_f32 v[58:59], v[56:57], v[58:59], v[86:87] op_sel_hi:[1,0,1]
	ds_write2_b64 v74, v[60:61], v[58:59] offset0:32 offset1:48
	v_pk_mul_f32 v[58:59], v[16:17], v[56:57] op_sel:[1,1] op_sel_hi:[0,1] neg_lo:[0,1]
	v_pk_fma_f32 v[56:57], v[16:17], v[56:57], v[58:59] op_sel_hi:[1,0,1]
	s_nop 0
	v_pk_mul_f32 v[58:59], v[56:57], v[104:105] op_sel:[1,1] op_sel_hi:[0,1] neg_lo:[0,1]
	v_pk_mul_f32 v[60:61], v[16:17], v[56:57] op_sel:[1,1] op_sel_hi:[0,1] neg_lo:[0,1]
	v_pk_fma_f32 v[58:59], v[56:57], v[104:105], v[58:59] op_sel_hi:[1,0,1]
	v_pk_fma_f32 v[56:57], v[16:17], v[56:57], v[60:61] op_sel_hi:[1,0,1]
	s_nop 0
	v_pk_mul_f32 v[60:61], v[56:57], v[82:83] op_sel:[1,1] op_sel_hi:[0,1] neg_lo:[0,1]
	v_pk_fma_f32 v[60:61], v[56:57], v[82:83], v[60:61] op_sel_hi:[1,0,1]
	ds_write2_b64 v73, v[58:59], v[60:61] offset0:64 offset1:80
	v_pk_mul_f32 v[58:59], v[16:17], v[56:57] op_sel:[1,1] op_sel_hi:[0,1] neg_lo:[0,1]
	v_pk_fma_f32 v[56:57], v[16:17], v[56:57], v[58:59] op_sel_hi:[1,0,1]
	s_nop 0
	v_pk_mul_f32 v[58:59], v[56:57], v[98:99] op_sel:[1,1] op_sel_hi:[0,1] neg_lo:[0,1]
	v_pk_mul_f32 v[60:61], v[16:17], v[56:57] op_sel:[1,1] op_sel_hi:[0,1] neg_lo:[0,1]
	v_pk_fma_f32 v[58:59], v[56:57], v[98:99], v[58:59] op_sel_hi:[1,0,1]
	v_pk_fma_f32 v[56:57], v[16:17], v[56:57], v[60:61] op_sel_hi:[1,0,1]
	s_nop 0
	v_pk_mul_f32 v[60:61], v[56:57], v[92:93] op_sel:[1,1] op_sel_hi:[0,1] neg_lo:[0,1]
	v_pk_fma_f32 v[60:61], v[56:57], v[92:93], v[60:61] op_sel_hi:[1,0,1]
	ds_write2_b64 v72, v[58:59], v[60:61] offset0:96 offset1:112
	v_pk_mul_f32 v[58:59], v[16:17], v[56:57] op_sel:[1,1] op_sel_hi:[0,1] neg_lo:[0,1]
	v_pk_fma_f32 v[56:57], v[16:17], v[56:57], v[58:59] op_sel_hi:[1,0,1]
	s_nop 0
	v_pk_mul_f32 v[58:59], v[56:57], v[46:47] op_sel:[1,1] op_sel_hi:[0,1] neg_lo:[0,1]
	v_pk_fma_f32 v[46:47], v[56:57], v[46:47], v[58:59] op_sel_hi:[1,0,1]
	v_pk_mul_f32 v[58:59], v[16:17], v[56:57] op_sel:[1,1] op_sel_hi:[0,1] neg_lo:[0,1]
	v_pk_fma_f32 v[56:57], v[16:17], v[56:57], v[58:59] op_sel_hi:[1,0,1]
	s_nop 0
	v_pk_mul_f32 v[58:59], v[56:57], v[90:91] op_sel:[1,1] op_sel_hi:[0,1] neg_lo:[0,1]
	v_pk_fma_f32 v[58:59], v[56:57], v[90:91], v[58:59] op_sel_hi:[1,0,1]
	ds_write2_b64 v71, v[46:47], v[58:59] offset0:128 offset1:144
	v_pk_mul_f32 v[46:47], v[16:17], v[56:57] op_sel:[1,1] op_sel_hi:[0,1] neg_lo:[0,1]
	v_pk_fma_f32 v[46:47], v[16:17], v[56:57], v[46:47] op_sel_hi:[1,0,1]
	s_nop 0
	v_pk_mul_f32 v[56:57], v[46:47], v[50:51] op_sel:[1,1] op_sel_hi:[0,1] neg_lo:[0,1]
	v_pk_fma_f32 v[50:51], v[46:47], v[50:51], v[56:57] op_sel_hi:[1,0,1]
	v_pk_mul_f32 v[56:57], v[16:17], v[46:47] op_sel:[1,1] op_sel_hi:[0,1] neg_lo:[0,1]
	v_pk_fma_f32 v[46:47], v[16:17], v[46:47], v[56:57] op_sel_hi:[1,0,1]
	s_nop 0
	v_pk_mul_f32 v[56:57], v[46:47], v[54:55] op_sel:[1,1] op_sel_hi:[0,1] neg_lo:[0,1]
	v_pk_fma_f32 v[54:55], v[46:47], v[54:55], v[56:57] op_sel_hi:[1,0,1]
	ds_write2_b64 v70, v[50:51], v[54:55] offset0:160 offset1:176
	v_pk_mul_f32 v[50:51], v[16:17], v[46:47] op_sel:[1,1] op_sel_hi:[0,1] neg_lo:[0,1]
	v_pk_fma_f32 v[46:47], v[16:17], v[46:47], v[50:51] op_sel_hi:[1,0,1]
	s_nop 0
	v_pk_mul_f32 v[50:51], v[38:39], v[46:47] op_sel:[1,1] op_sel_hi:[1,0] neg_lo:[1,0]
	s_nop 0
	v_pk_fma_f32 v[38:39], v[38:39], v[46:47], v[50:51] op_sel_hi:[0,1,1]
	v_pk_mul_f32 v[50:51], v[16:17], v[46:47] op_sel:[1,1] op_sel_hi:[0,1] neg_lo:[0,1]
	v_pk_fma_f32 v[46:47], v[16:17], v[46:47], v[50:51] op_sel_hi:[1,0,1]
	s_nop 0
	v_pk_mul_f32 v[50:51], v[46:47], v[76:77] op_sel:[1,1] op_sel_hi:[0,1] neg_lo:[0,1]
	v_pk_fma_f32 v[50:51], v[46:47], v[76:77], v[50:51] op_sel_hi:[1,0,1]
	ds_write2_b64 v69, v[38:39], v[50:51] offset0:192 offset1:208
	v_pk_mul_f32 v[38:39], v[16:17], v[46:47] op_sel:[1,1] op_sel_hi:[0,1] neg_lo:[0,1]
	v_pk_fma_f32 v[38:39], v[16:17], v[46:47], v[38:39] op_sel_hi:[1,0,1]
	s_nop 0
	v_pk_mul_f32 v[46:47], v[42:43], v[38:39] op_sel:[1,1] op_sel_hi:[1,0] neg_lo:[1,0]
	s_nop 0
	v_pk_fma_f32 v[42:43], v[42:43], v[38:39], v[46:47] op_sel_hi:[0,1,1]
	v_pk_mul_f32 v[46:47], v[16:17], v[38:39] op_sel:[1,1] op_sel_hi:[0,1] neg_lo:[0,1]
	v_pk_fma_f32 v[38:39], v[16:17], v[38:39], v[46:47] op_sel_hi:[1,0,1]
	s_nop 0
	v_pk_mul_f32 v[46:47], v[38:39], v[84:85] op_sel:[1,1] op_sel_hi:[0,1] neg_lo:[0,1]
	v_pk_fma_f32 v[46:47], v[38:39], v[84:85], v[46:47] op_sel_hi:[1,0,1]
	ds_write2_b64 v68, v[42:43], v[46:47] offset0:224 offset1:240
	v_pk_mul_f32 v[42:43], v[16:17], v[38:39] op_sel:[1,1] op_sel_hi:[0,1] neg_lo:[0,1]
	v_pk_fma_f32 v[38:39], v[16:17], v[38:39], v[42:43] op_sel_hi:[1,0,1]
	s_nop 0
	v_pk_mul_f32 v[42:43], v[30:31], v[38:39] op_sel:[1,1] op_sel_hi:[1,0] neg_lo:[1,0]
	s_nop 0
	v_pk_fma_f32 v[30:31], v[30:31], v[38:39], v[42:43] op_sel_hi:[0,1,1]
	v_pk_mul_f32 v[42:43], v[16:17], v[38:39] op_sel:[1,1] op_sel_hi:[0,1] neg_lo:[0,1]
	v_pk_fma_f32 v[38:39], v[16:17], v[38:39], v[42:43] op_sel_hi:[1,0,1]
	s_nop 0
	v_pk_mul_f32 v[42:43], v[78:79], v[38:39] op_sel:[1,1] op_sel_hi:[1,0] neg_lo:[1,0]
	s_nop 0
	v_pk_fma_f32 v[42:43], v[78:79], v[38:39], v[42:43] op_sel_hi:[0,1,1]
	ds_write2_b64 v67, v[30:31], v[42:43] offset1:16
	v_pk_mul_f32 v[30:31], v[16:17], v[38:39] op_sel:[1,1] op_sel_hi:[0,1] neg_lo:[0,1]
	v_pk_fma_f32 v[30:31], v[16:17], v[38:39], v[30:31] op_sel_hi:[1,0,1]
	s_nop 0
	v_pk_mul_f32 v[38:39], v[34:35], v[30:31] op_sel:[1,1] op_sel_hi:[1,0] neg_lo:[1,0]
	s_nop 0
	v_pk_fma_f32 v[34:35], v[34:35], v[30:31], v[38:39] op_sel_hi:[0,1,1]
	v_pk_mul_f32 v[38:39], v[16:17], v[30:31] op_sel:[1,1] op_sel_hi:[0,1] neg_lo:[0,1]
	v_pk_fma_f32 v[30:31], v[16:17], v[30:31], v[38:39] op_sel_hi:[1,0,1]
	s_nop 0
	v_pk_mul_f32 v[38:39], v[52:53], v[30:31] op_sel:[1,1] op_sel_hi:[1,0] neg_lo:[1,0]
	s_nop 0
	v_pk_fma_f32 v[38:39], v[52:53], v[30:31], v[38:39] op_sel_hi:[0,1,1]
	ds_write2_b64 v66, v[34:35], v[38:39] offset0:32 offset1:48
	v_pk_mul_f32 v[34:35], v[16:17], v[30:31] op_sel:[1,1] op_sel_hi:[0,1] neg_lo:[0,1]
	v_pk_fma_f32 v[30:31], v[16:17], v[30:31], v[34:35] op_sel_hi:[1,0,1]
	s_nop 0
	v_pk_mul_f32 v[34:35], v[26:27], v[30:31] op_sel:[1,1] op_sel_hi:[1,0] neg_lo:[1,0]
	s_nop 0
	v_pk_fma_f32 v[26:27], v[26:27], v[30:31], v[34:35] op_sel_hi:[0,1,1]
	v_pk_mul_f32 v[34:35], v[16:17], v[30:31] op_sel:[1,1] op_sel_hi:[0,1] neg_lo:[0,1]
	v_pk_fma_f32 v[30:31], v[16:17], v[30:31], v[34:35] op_sel_hi:[1,0,1]
	s_nop 0
	v_pk_mul_f32 v[34:35], v[48:49], v[30:31] op_sel:[1,1] op_sel_hi:[1,0] neg_lo:[1,0]
	s_nop 0
	v_pk_fma_f32 v[34:35], v[48:49], v[30:31], v[34:35] op_sel_hi:[0,1,1]
	ds_write2_b64 v65, v[26:27], v[34:35] offset0:64 offset1:80
	v_pk_mul_f32 v[26:27], v[16:17], v[30:31] op_sel:[1,1] op_sel_hi:[0,1] neg_lo:[0,1]
	v_pk_fma_f32 v[26:27], v[16:17], v[30:31], v[26:27] op_sel_hi:[1,0,1]
	s_nop 0
	v_pk_mul_f32 v[30:31], v[28:29], v[26:27] op_sel:[1,1] op_sel_hi:[1,0] neg_lo:[1,0]
	s_nop 0
	v_pk_fma_f32 v[28:29], v[28:29], v[26:27], v[30:31] op_sel_hi:[0,1,1]
	v_pk_mul_f32 v[30:31], v[16:17], v[26:27] op_sel:[1,1] op_sel_hi:[0,1] neg_lo:[0,1]
	v_pk_fma_f32 v[26:27], v[16:17], v[26:27], v[30:31] op_sel_hi:[1,0,1]
	s_nop 0
	v_pk_mul_f32 v[30:31], v[80:81], v[26:27] op_sel:[1,1] op_sel_hi:[1,0] neg_lo:[1,0]
	s_nop 0
	v_pk_fma_f32 v[30:31], v[80:81], v[26:27], v[30:31] op_sel_hi:[0,1,1]
	ds_write2_b64 v64, v[28:29], v[30:31] offset0:96 offset1:112
	v_pk_mul_f32 v[28:29], v[16:17], v[26:27] op_sel:[1,1] op_sel_hi:[0,1] neg_lo:[0,1]
	v_pk_fma_f32 v[26:27], v[16:17], v[26:27], v[28:29] op_sel_hi:[1,0,1]
	s_nop 0
	v_pk_mul_f32 v[28:29], v[22:23], v[26:27] op_sel:[1,1] op_sel_hi:[1,0] neg_lo:[1,0]
	s_nop 0
	v_pk_fma_f32 v[22:23], v[22:23], v[26:27], v[28:29] op_sel_hi:[0,1,1]
	v_pk_mul_f32 v[28:29], v[16:17], v[26:27] op_sel:[1,1] op_sel_hi:[0,1] neg_lo:[0,1]
	v_pk_fma_f32 v[26:27], v[16:17], v[26:27], v[28:29] op_sel_hi:[1,0,1]
	s_nop 0
	v_pk_mul_f32 v[28:29], v[40:41], v[26:27] op_sel:[1,1] op_sel_hi:[1,0] neg_lo:[1,0]
	s_nop 0
	v_pk_fma_f32 v[28:29], v[40:41], v[26:27], v[28:29] op_sel_hi:[0,1,1]
	ds_write2_b64 v63, v[22:23], v[28:29] offset0:128 offset1:144
	v_pk_mul_f32 v[22:23], v[16:17], v[26:27] op_sel:[1,1] op_sel_hi:[0,1] neg_lo:[0,1]
	v_pk_fma_f32 v[22:23], v[16:17], v[26:27], v[22:23] op_sel_hi:[1,0,1]
	s_nop 0
	v_pk_mul_f32 v[26:27], v[24:25], v[22:23] op_sel:[1,1] op_sel_hi:[1,0] neg_lo:[1,0]
	s_nop 0
	v_pk_fma_f32 v[24:25], v[24:25], v[22:23], v[26:27] op_sel_hi:[0,1,1]
	v_pk_mul_f32 v[26:27], v[16:17], v[22:23] op_sel:[1,1] op_sel_hi:[0,1] neg_lo:[0,1]
	v_pk_fma_f32 v[22:23], v[16:17], v[22:23], v[26:27] op_sel_hi:[1,0,1]
	s_nop 0
	v_pk_mul_f32 v[26:27], v[44:45], v[22:23] op_sel:[1,1] op_sel_hi:[1,0] neg_lo:[1,0]
	s_nop 0
	v_pk_fma_f32 v[26:27], v[44:45], v[22:23], v[26:27] op_sel_hi:[0,1,1]
	ds_write2_b64 v62, v[24:25], v[26:27] offset0:160 offset1:176
	v_pk_mul_f32 v[24:25], v[16:17], v[22:23] op_sel:[1,1] op_sel_hi:[0,1] neg_lo:[0,1]
	v_pk_fma_f32 v[22:23], v[16:17], v[22:23], v[24:25] op_sel_hi:[1,0,1]
	s_nop 0
	v_pk_mul_f32 v[24:25], v[18:19], v[22:23] op_sel:[1,1] op_sel_hi:[1,0] neg_lo:[1,0]
	s_nop 0
	v_pk_fma_f32 v[18:19], v[18:19], v[22:23], v[24:25] op_sel_hi:[0,1,1]
	v_pk_mul_f32 v[24:25], v[16:17], v[22:23] op_sel:[1,1] op_sel_hi:[0,1] neg_lo:[0,1]
	v_pk_fma_f32 v[22:23], v[16:17], v[22:23], v[24:25] op_sel_hi:[1,0,1]
	s_nop 0
	v_pk_mul_f32 v[24:25], v[32:33], v[22:23] op_sel:[1,1] op_sel_hi:[1,0] neg_lo:[1,0]
	s_nop 0
	v_pk_fma_f32 v[24:25], v[32:33], v[22:23], v[24:25] op_sel_hi:[0,1,1]
	ds_write2_b64 v15, v[18:19], v[24:25] offset0:192 offset1:208
	v_pk_mul_f32 v[18:19], v[16:17], v[22:23] op_sel:[1,1] op_sel_hi:[0,1] neg_lo:[0,1]
	v_pk_fma_f32 v[18:19], v[16:17], v[22:23], v[18:19] op_sel_hi:[1,0,1]
	s_nop 0
	v_pk_mul_f32 v[22:23], v[20:21], v[18:19] op_sel:[1,1] op_sel_hi:[1,0] neg_lo:[1,0]
	s_nop 0
	v_pk_fma_f32 v[20:21], v[20:21], v[18:19], v[22:23] op_sel_hi:[0,1,1]
	v_pk_mul_f32 v[22:23], v[16:17], v[18:19] op_sel:[1,1] op_sel_hi:[0,1] neg_lo:[0,1]
	v_pk_fma_f32 v[16:17], v[16:17], v[18:19], v[22:23] op_sel_hi:[1,0,1]
	s_nop 0
	v_pk_mul_f32 v[18:19], v[36:37], v[16:17] op_sel:[1,1] op_sel_hi:[1,0] neg_lo:[1,0]
	s_nop 0
	v_pk_fma_f32 v[16:17], v[36:37], v[16:17], v[18:19] op_sel_hi:[0,1,1]
	ds_write2_b64 v13, v[20:21], v[16:17] offset0:224 offset1:240
	v_mov_b32_e32 v16, v1
	v_mov_b32_e32 v10, v178
	v_mov_b32_e32 v17, v177
	s_waitcnt lgkmcnt(0)
	s_barrier
	v_lshlrev_b32_e32 v190, 3, v16
	v_add_u32_e32 v190, 0x1000, v190
	global_load_dwordx2 v[196:197], v190, s[48:49] offset:-4096
	global_load_dwordx2 v[198:199], v190, s[48:49]
	v_add_u32_e32 v190, 0x2000, v190
	global_load_dwordx2 v[200:201], v190, s[48:49] offset:-4096
	global_load_dwordx2 v[202:203], v190, s[48:49]
	v_add_u32_e32 v190, 0x2000, v190
	global_load_dwordx2 v[204:205], v190, s[48:49] offset:-4096
	global_load_dwordx2 v[206:207], v190, s[48:49]
	v_add_u32_e32 v190, 0x2000, v190
	global_load_dwordx2 v[208:209], v190, s[48:49] offset:-4096
	global_load_dwordx2 v[210:211], v190, s[48:49]
	v_add_u32_e32 v190, 0x2000, v190
	global_load_dwordx2 v[212:213], v190, s[48:49] offset:-4096
	global_load_dwordx2 v[214:215], v190, s[48:49]
	v_add_u32_e32 v190, 0x2000, v190
	global_load_dwordx2 v[216:217], v190, s[48:49] offset:-4096
	global_load_dwordx2 v[218:219], v190, s[48:49]
	v_add_u32_e32 v190, 0x2000, v190
	global_load_dwordx2 v[220:221], v190, s[48:49] offset:-4096
	global_load_dwordx2 v[222:223], v190, s[48:49]
	v_add_u32_e32 v190, 0x2000, v190
	global_load_dwordx2 v[224:225], v190, s[48:49] offset:-4096
	global_load_dwordx2 v[226:227], v190, s[48:49]
	v_mov_b32_e32 v50, v166
	v_lshlrev_b32_e32 v13, 3, v17
	v_lshlrev_b32_e32 v48, 3, v10
	v_add3_u32 v10, 0, v13, v48
	v_xor_b32_e32 v13, 1, v17
	v_xor_b32_e32 v34, 8, v17
	v_xor_b32_e32 v36, 9, v17
	v_lshlrev_b32_e32 v13, 3, v13
	v_xor_b32_e32 v15, 2, v17
	v_xor_b32_e32 v24, 3, v17
	v_xor_b32_e32 v26, 4, v17
	v_xor_b32_e32 v28, 5, v17
	v_xor_b32_e32 v30, 6, v17
	v_xor_b32_e32 v32, 7, v17
	v_lshlrev_b32_e32 v34, 3, v34
	v_lshlrev_b32_e32 v36, 3, v36
	v_xor_b32_e32 v38, 10, v17
	v_xor_b32_e32 v40, 11, v17
	v_xor_b32_e32 v42, 12, v17
	v_xor_b32_e32 v44, 13, v17
	v_xor_b32_e32 v46, 14, v17
	v_xor_b32_e32 v17, 15, v17
	v_add3_u32 v13, 0, v13, v48
	v_lshlrev_b32_e32 v15, 3, v15
	v_lshlrev_b32_e32 v24, 3, v24
	v_lshlrev_b32_e32 v26, 3, v26
	v_lshlrev_b32_e32 v28, 3, v28
	v_lshlrev_b32_e32 v30, 3, v30
	v_lshlrev_b32_e32 v32, 3, v32
	v_add3_u32 v57, 0, v34, v48
	v_add3_u32 v58, 0, v36, v48
	v_lshlrev_b32_e32 v38, 3, v38
	v_lshlrev_b32_e32 v40, 3, v40
	v_lshlrev_b32_e32 v42, 3, v42
	v_lshlrev_b32_e32 v44, 3, v44
	v_lshlrev_b32_e32 v46, 3, v46
	v_lshlrev_b32_e32 v17, 3, v17
	ds_read_b64 v[18:19], v10
	ds_read_b64 v[20:21], v13
	v_add3_u32 v15, 0, v15, v48
	v_add3_u32 v52, 0, v24, v48
	v_add3_u32 v53, 0, v26, v48
	v_add3_u32 v54, 0, v28, v48
	v_add3_u32 v55, 0, v30, v48
	v_add3_u32 v56, 0, v32, v48
	ds_read_b64 v[34:35], v57
	ds_read_b64 v[36:37], v58
	v_add3_u32 v59, 0, v38, v48
	v_add3_u32 v60, 0, v40, v48
	v_add3_u32 v61, 0, v42, v48
	v_add3_u32 v62, 0, v44, v48
	v_add3_u32 v63, 0, v46, v48
	v_add3_u32 v64, 0, v17, v48
	v_mov_b32_e32 v17, v164
	ds_read_b64 v[22:23], v15
	ds_read_b64 v[24:25], v52
	ds_read_b64 v[26:27], v53
	ds_read_b64 v[28:29], v54
	ds_read_b64 v[30:31], v55
	ds_read_b64 v[32:33], v56
	ds_read_b64 v[38:39], v59
	ds_read_b64 v[40:41], v60
	ds_read_b64 v[42:43], v61
	ds_read_b64 v[44:45], v62
	ds_read_b64 v[46:47], v63
	ds_read_b64 v[48:49], v64
	s_waitcnt lgkmcnt(13)
	v_pk_add_f32 v[70:71], v[18:19], v[34:35]
	v_mov_b32_e32 v17, v165
	v_pk_add_f32 v[18:19], v[18:19], v[34:35] neg_lo:[0,1] neg_hi:[0,1]
	v_mov_b32_e32 v17, v167
	s_waitcnt lgkmcnt(12)
	v_pk_add_f32 v[34:35], v[20:21], v[36:37]
	v_pk_add_f32 v[20:21], v[20:21], v[36:37] neg_lo:[0,1] neg_hi:[0,1]
	v_mov_b32_e32 v66, v168
	v_mov_b32_e32 v17, v169
	v_mov_b32_e32 v68, v170
	s_nop 0
	v_pk_mul_f32 v[36:37], v[20:21], v[68:69] op_sel:[1,0] op_sel_hi:[0,0] neg_lo:[1,1] neg_hi:[0,1]
	v_mov_b32_e32 v17, v171
	v_pk_fma_f32 v[20:21], v[20:21], v[50:51], v[36:37] op_sel_hi:[1,0,1]
	s_waitcnt lgkmcnt(5)
	v_pk_add_f32 v[36:37], v[22:23], v[38:39]
	v_pk_add_f32 v[22:23], v[22:23], v[38:39] neg_lo:[0,1] neg_hi:[0,1]
	s_nop 0
	v_pk_mul_f32 v[38:39], v[22:23], v[66:67] op_sel:[1,0] op_sel_hi:[0,0] neg_lo:[1,1] neg_hi:[0,1]
	v_mov_b32_e32 v17, v172
	v_pk_fma_f32 v[22:23], v[22:23], v[66:67], v[38:39] op_sel_hi:[1,0,1]
	s_waitcnt lgkmcnt(4)
	v_pk_add_f32 v[38:39], v[24:25], v[40:41]
	v_pk_add_f32 v[24:25], v[24:25], v[40:41] neg_lo:[0,1] neg_hi:[0,1]
	s_nop 0
	v_pk_mul_f32 v[40:41], v[24:25], v[68:69] op_sel_hi:[1,0]
	s_nop 0
	v_pk_fma_f32 v[24:25], v[24:25], v[50:51], v[40:41] op_sel:[1,0,0] op_sel_hi:[0,0,1] neg_lo:[1,1,0] neg_hi:[0,1,0]
	s_waitcnt lgkmcnt(3)
	v_pk_add_f32 v[40:41], v[26:27], v[42:43]
	v_pk_add_f32 v[26:27], v[26:27], v[42:43] neg_lo:[0,1] neg_hi:[0,1]
	v_ashrrev_i32_e32 v17, 31, v16
	v_xor_b32_e32 v73, 0x80000000, v26
	v_mov_b32_e32 v72, v27
	s_waitcnt lgkmcnt(2)
	v_pk_add_f32 v[26:27], v[28:29], v[44:45]
	v_pk_add_f32 v[28:29], v[28:29], v[44:45] neg_lo:[0,1] neg_hi:[0,1]
	s_nop 0
	v_pk_mul_f32 v[42:43], v[28:29], v[68:69] op_sel_hi:[1,0] neg_lo:[0,1] neg_hi:[0,1]
	s_nop 0
	v_pk_fma_f32 v[28:29], v[28:29], v[50:51], v[42:43] op_sel:[1,0,0] op_sel_hi:[0,0,1] neg_lo:[1,1,0] neg_hi:[0,1,0]
	s_waitcnt lgkmcnt(1)
	v_pk_add_f32 v[42:43], v[30:31], v[46:47]
	v_pk_add_f32 v[30:31], v[30:31], v[46:47] neg_lo:[0,1] neg_hi:[0,1]
	s_nop 0
	v_pk_mul_f32 v[44:45], v[30:31], v[66:67] op_sel:[1,0] op_sel_hi:[0,0] neg_lo:[1,1] neg_hi:[0,1]
	s_nop 0
	v_pk_fma_f32 v[30:31], v[30:31], v[66:67], v[44:45] op_sel_hi:[1,0,1] neg_lo:[0,1,0] neg_hi:[0,1,0]
	s_waitcnt lgkmcnt(0)
	v_pk_add_f32 v[44:45], v[32:33], v[48:49]
	v_pk_add_f32 v[32:33], v[32:33], v[48:49] neg_lo:[0,1] neg_hi:[0,1]
	v_pk_add_f32 v[48:49], v[34:35], v[26:27]
	v_pk_add_f32 v[26:27], v[34:35], v[26:27] neg_lo:[0,1] neg_hi:[0,1]
	s_nop 0
	v_pk_mul_f32 v[34:35], v[26:27], v[66:67] op_sel:[1,0] op_sel_hi:[0,0] neg_lo:[1,1] neg_hi:[0,1]
	v_pk_fma_f32 v[26:27], v[26:27], v[66:67], v[34:35] op_sel_hi:[1,0,1]
	v_pk_add_f32 v[34:35], v[36:37], v[42:43]
	v_pk_add_f32 v[36:37], v[36:37], v[42:43] neg_lo:[0,1] neg_hi:[0,1]
	v_pk_mul_f32 v[46:47], v[32:33], v[68:69] op_sel:[1,0] op_sel_hi:[0,0] neg_lo:[1,1] neg_hi:[0,1]
	v_xor_b32_e32 v43, 0x80000000, v36
	v_mov_b32_e32 v42, v37
	v_pk_add_f32 v[36:37], v[38:39], v[44:45]
	v_pk_add_f32 v[38:39], v[38:39], v[44:45] neg_lo:[0,1] neg_hi:[0,1]
	v_pk_fma_f32 v[46:47], v[32:33], v[50:51], v[46:47] op_sel_hi:[1,0,1] neg_lo:[0,1,0] neg_hi:[0,1,0]
	v_pk_add_f32 v[32:33], v[70:71], v[40:41]
	v_pk_mul_f32 v[44:45], v[38:39], v[66:67] op_sel:[1,0] op_sel_hi:[0,0] neg_lo:[1,1] neg_hi:[0,1]
	v_pk_add_f32 v[40:41], v[70:71], v[40:41] neg_lo:[0,1] neg_hi:[0,1]
	v_pk_fma_f32 v[38:39], v[38:39], v[66:67], v[44:45] op_sel_hi:[1,0,1] neg_lo:[0,1,0] neg_hi:[0,1,0]
	v_pk_add_f32 v[44:45], v[32:33], v[34:35]
	v_pk_add_f32 v[32:33], v[32:33], v[34:35] neg_lo:[0,1] neg_hi:[0,1]
	v_pk_add_f32 v[34:35], v[48:49], v[36:37]
	v_pk_add_f32 v[36:37], v[48:49], v[36:37] neg_lo:[0,1] neg_hi:[0,1]
	v_pk_add_f32 v[50:51], v[44:45], v[34:35]
	v_xor_b32_e32 v49, 0x80000000, v36
	v_mov_b32_e32 v48, v37
	v_pk_add_f32 v[36:37], v[44:45], v[34:35] neg_lo:[0,1] neg_hi:[0,1]
	v_pk_add_f32 v[68:69], v[32:33], v[48:49]
	v_pk_add_f32 v[44:45], v[32:33], v[48:49] neg_lo:[0,1] neg_hi:[0,1]
	v_pk_add_f32 v[32:33], v[40:41], v[42:43]
	v_pk_add_f32 v[34:35], v[40:41], v[42:43] neg_lo:[0,1] neg_hi:[0,1]
	v_pk_add_f32 v[40:41], v[26:27], v[38:39]
	v_pk_add_f32 v[26:27], v[26:27], v[38:39] neg_lo:[0,1] neg_hi:[0,1]
	v_pk_add_f32 v[42:43], v[32:33], v[40:41] neg_lo:[0,1] neg_hi:[0,1]
	v_xor_b32_e32 v39, 0x80000000, v26
	v_mov_b32_e32 v38, v27
	v_pk_add_f32 v[26:27], v[32:33], v[40:41]
	v_pk_add_f32 v[40:41], v[20:21], v[28:29]
	v_pk_add_f32 v[20:21], v[20:21], v[28:29] neg_lo:[0,1] neg_hi:[0,1]
	v_pk_add_f32 v[32:33], v[34:35], v[38:39]
	v_pk_mul_f32 v[28:29], v[66:67], v[20:21] op_sel:[0,1] op_sel_hi:[0,0] neg_lo:[1,1] neg_hi:[1,0]
	v_pk_fma_f32 v[20:21], v[66:67], v[20:21], v[28:29] op_sel_hi:[0,1,1]
	v_pk_add_f32 v[28:29], v[22:23], v[30:31]
	v_pk_add_f32 v[22:23], v[22:23], v[30:31] neg_lo:[0,1] neg_hi:[0,1]
	v_pk_add_f32 v[38:39], v[34:35], v[38:39] neg_lo:[0,1] neg_hi:[0,1]
	v_xor_b32_e32 v31, 0x80000000, v22
	v_mov_b32_e32 v30, v23
	v_pk_add_f32 v[22:23], v[24:25], v[46:47]
	v_pk_add_f32 v[24:25], v[24:25], v[46:47] neg_lo:[0,1] neg_hi:[0,1]
	v_pk_add_f32 v[34:35], v[18:19], v[72:73]
	v_pk_mul_f32 v[46:47], v[66:67], v[24:25] op_sel:[0,1] op_sel_hi:[0,0] neg_lo:[1,1] neg_hi:[1,0]
	v_pk_fma_f32 v[24:25], v[66:67], v[24:25], v[46:47] op_sel_hi:[0,1,1] neg_lo:[1,0,0] neg_hi:[1,0,0]
	v_pk_add_f32 v[46:47], v[34:35], v[28:29]
	v_pk_add_f32 v[28:29], v[34:35], v[28:29] neg_lo:[0,1] neg_hi:[0,1]
	v_pk_add_f32 v[34:35], v[40:41], v[22:23]
	v_pk_add_f32 v[22:23], v[40:41], v[22:23] neg_lo:[0,1] neg_hi:[0,1]
	v_pk_add_f32 v[18:19], v[18:19], v[72:73] neg_lo:[0,1] neg_hi:[0,1]
	v_pk_add_f32 v[66:67], v[28:29], v[22:23] op_sel:[0,1] op_sel_hi:[1,0] neg_hi:[0,1]
	v_pk_add_f32 v[48:49], v[28:29], v[22:23] op_sel:[0,1] op_sel_hi:[1,0] neg_lo:[0,1]
	v_pk_add_f32 v[28:29], v[18:19], v[30:31]
	v_pk_add_f32 v[18:19], v[18:19], v[30:31] neg_lo:[0,1] neg_hi:[0,1]
	v_pk_add_f32 v[30:31], v[20:21], v[24:25]
	v_pk_add_f32 v[20:21], v[20:21], v[24:25] neg_lo:[0,1] neg_hi:[0,1]
	v_pk_add_f32 v[22:23], v[46:47], v[34:35]
	v_xor_b32_e32 v25, 0x80000000, v20
	v_mov_b32_e32 v24, v21
	v_lshl_add_u64 v[20:21], v[16:17], 3, s[48:49]
	s_waitcnt vmcnt(0)
	v_pk_add_f32 v[40:41], v[46:47], v[34:35] neg_lo:[0,1] neg_hi:[0,1]
	v_pk_add_f32 v[34:35], v[18:19], v[24:25]
	v_pk_add_f32 v[18:19], v[18:19], v[24:25] neg_lo:[0,1] neg_hi:[0,1]
	v_pk_add_f32 v[70:71], v[28:29], v[30:31]
	v_pk_add_f32 v[46:47], v[28:29], v[30:31] neg_lo:[0,1] neg_hi:[0,1]
	v_mov_b32_e32 v17, v164
	s_nop 0
	v_pk_mul_f32 v[24:25], v[50:51], v[196:197] op_sel:[1,1] op_sel_hi:[1,0] neg_lo:[1,0]
	s_nop 0
	v_pk_fma_f32 v[20:21], v[50:51], v[196:197], v[24:25] op_sel_hi:[0,1,1]
	v_add_u32_e32 v24, 0x200, v16
	v_ashrrev_i32_e32 v25, 31, v24
	v_lshl_add_u64 v[24:25], v[24:25], 3, s[48:49]
	s_nop 0
	v_pk_mul_f32 v[28:29], v[198:199], v[22:23] op_sel:[1,1] op_sel_hi:[0,1] neg_lo:[0,1]
	v_pk_fma_f32 v[22:23], v[198:199], v[22:23], v[28:29] op_sel_hi:[1,0,1]
	v_add_u32_e32 v24, 0x400, v16
	v_ashrrev_i32_e32 v25, 31, v24
	v_lshl_add_u64 v[24:25], v[24:25], 3, s[48:49]
	s_nop 0
	v_pk_mul_f32 v[28:29], v[26:27], v[200:201] op_sel:[1,1] op_sel_hi:[1,0] neg_lo:[1,0]
	s_nop 0
	v_pk_fma_f32 v[24:25], v[26:27], v[200:201], v[28:29] op_sel_hi:[0,1,1]
	v_add_u32_e32 v26, 0x600, v16
	v_ashrrev_i32_e32 v27, 31, v26
	v_lshl_add_u64 v[26:27], v[26:27], 3, s[48:49]
	s_nop 0
	v_pk_mul_f32 v[28:29], v[202:203], v[70:71] op_sel:[1,1] op_sel_hi:[0,1] neg_lo:[0,1]
	v_pk_fma_f32 v[26:27], v[202:203], v[70:71], v[28:29] op_sel_hi:[1,0,1]
	v_add_u32_e32 v28, 0x800, v16
	v_ashrrev_i32_e32 v29, 31, v28
	v_lshl_add_u64 v[28:29], v[28:29], 3, s[48:49]
	s_nop 0
	v_pk_mul_f32 v[30:31], v[68:69], v[204:205] op_sel:[1,1] op_sel_hi:[1,0] neg_lo:[1,0]
	s_nop 0
	v_pk_fma_f32 v[28:29], v[68:69], v[204:205], v[30:31] op_sel_hi:[0,1,1]
	v_add_u32_e32 v30, 0xa00, v16
	v_ashrrev_i32_e32 v31, 31, v30
	v_lshl_add_u64 v[30:31], v[30:31], 3, s[48:49]
	v_mov_b32_e32 v68, v170
	s_nop 0
	v_pk_mul_f32 v[50:51], v[206:207], v[66:67] op_sel:[1,1] op_sel_hi:[0,1] neg_lo:[0,1]
	v_pk_fma_f32 v[30:31], v[206:207], v[66:67], v[50:51] op_sel_hi:[1,0,1]
	v_add_u32_e32 v50, 0xc00, v16
	v_ashrrev_i32_e32 v51, 31, v50
	v_lshl_add_u64 v[50:51], v[50:51], 3, s[48:49]
	s_nop 0
	v_pk_mul_f32 v[66:67], v[32:33], v[208:209] op_sel:[1,1] op_sel_hi:[1,0] neg_lo:[1,0]
	s_nop 0
	v_pk_fma_f32 v[32:33], v[32:33], v[208:209], v[66:67] op_sel_hi:[0,1,1]
	v_add_u32_e32 v50, 0xe00, v16
	v_ashrrev_i32_e32 v51, 31, v50
	v_lshl_add_u64 v[50:51], v[50:51], 3, s[48:49]
	s_nop 0
	v_pk_mul_f32 v[66:67], v[210:211], v[34:35] op_sel:[1,1] op_sel_hi:[0,1] neg_lo:[0,1]
	v_pk_fma_f32 v[34:35], v[210:211], v[34:35], v[66:67] op_sel_hi:[1,0,1]
	v_add_u32_e32 v50, 0x1000, v16
	v_ashrrev_i32_e32 v51, 31, v50
	v_lshl_add_u64 v[50:51], v[50:51], 3, s[48:49]
	s_nop 0
	v_pk_mul_f32 v[66:67], v[36:37], v[212:213] op_sel:[1,1] op_sel_hi:[1,0] neg_lo:[1,0]
	s_nop 0
	v_pk_fma_f32 v[36:37], v[36:37], v[212:213], v[66:67] op_sel_hi:[0,1,1]
	v_add_u32_e32 v50, 0x1200, v16
	v_ashrrev_i32_e32 v51, 31, v50
	v_lshl_add_u64 v[50:51], v[50:51], 3, s[48:49]
	v_pk_add_f32 v[70:71], v[20:21], v[36:37]
	v_pk_add_f32 v[20:21], v[20:21], v[36:37] neg_lo:[0,1] neg_hi:[0,1]
	s_nop 0
	v_pk_mul_f32 v[66:67], v[40:41], v[214:215] op_sel:[1,1] op_sel_hi:[1,0] neg_lo:[1,0]
	s_nop 0
	v_pk_fma_f32 v[40:41], v[40:41], v[214:215], v[66:67] op_sel_hi:[0,1,1]
	v_add_u32_e32 v50, 0x1400, v16
	v_ashrrev_i32_e32 v51, 31, v50
	v_lshl_add_u64 v[50:51], v[50:51], 3, s[48:49]
	v_pk_add_f32 v[36:37], v[22:23], v[40:41]
	v_pk_add_f32 v[22:23], v[22:23], v[40:41] neg_lo:[0,1] neg_hi:[0,1]
	s_nop 0
	v_pk_mul_f32 v[66:67], v[42:43], v[216:217] op_sel:[1,1] op_sel_hi:[1,0] neg_lo:[1,0]
	s_nop 0
	v_pk_fma_f32 v[42:43], v[42:43], v[216:217], v[66:67] op_sel_hi:[0,1,1]
	v_add_u32_e32 v50, 0x1600, v16
	v_ashrrev_i32_e32 v51, 31, v50
	v_lshl_add_u64 v[50:51], v[50:51], 3, s[48:49]
	s_nop 0
	v_pk_mul_f32 v[66:67], v[46:47], v[218:219] op_sel:[1,1] op_sel_hi:[1,0] neg_lo:[1,0]
	s_nop 0
	v_pk_fma_f32 v[46:47], v[46:47], v[218:219], v[66:67] op_sel_hi:[0,1,1]
	v_add_u32_e32 v50, 0x1800, v16
	v_ashrrev_i32_e32 v51, 31, v50
	v_lshl_add_u64 v[50:51], v[50:51], 3, s[48:49]
	s_nop 0
	v_pk_mul_f32 v[66:67], v[44:45], v[220:221] op_sel:[1,1] op_sel_hi:[1,0] neg_lo:[1,0]
	s_nop 0
	v_pk_fma_f32 v[44:45], v[44:45], v[220:221], v[66:67] op_sel_hi:[0,1,1]
	v_add_u32_e32 v50, 0x1a00, v16
	v_ashrrev_i32_e32 v51, 31, v50
	v_lshl_add_u64 v[50:51], v[50:51], 3, s[48:49]
	s_nop 0
	v_pk_mul_f32 v[66:67], v[48:49], v[222:223] op_sel:[1,1] op_sel_hi:[1,0] neg_lo:[1,0]
	s_nop 0
	v_pk_fma_f32 v[48:49], v[48:49], v[222:223], v[66:67] op_sel_hi:[0,1,1]
	v_add_u32_e32 v50, 0x1c00, v16
	v_ashrrev_i32_e32 v51, 31, v50
	v_lshl_add_u64 v[50:51], v[50:51], 3, s[48:49]
	s_nop 0
	v_pk_mul_f32 v[66:67], v[38:39], v[224:225] op_sel:[1,1] op_sel_hi:[1,0] neg_lo:[1,0]
	s_nop 0
	v_pk_fma_f32 v[38:39], v[38:39], v[224:225], v[66:67] op_sel_hi:[0,1,1]
	v_add_u32_e32 v50, 0x1e00, v16
	v_ashrrev_i32_e32 v51, 31, v50
	v_lshl_add_u64 v[50:51], v[50:51], 3, s[48:49]
	v_mov_b32_e32 v50, v226
	v_mov_b32_e32 v51, v227
	v_lshlrev_b32_e32 v190, 3, v16
	v_add_u32_e32 v190, 0x11000, v190
	global_load_dwordx2 v[196:197], v190, s[48:49] offset:-4096
	global_load_dwordx2 v[198:199], v190, s[48:49]
	v_add_u32_e32 v190, 0x2000, v190
	global_load_dwordx2 v[200:201], v190, s[48:49] offset:-4096
	global_load_dwordx2 v[202:203], v190, s[48:49]
	v_add_u32_e32 v190, 0x2000, v190
	global_load_dwordx2 v[204:205], v190, s[48:49] offset:-4096
	global_load_dwordx2 v[206:207], v190, s[48:49]
	v_add_u32_e32 v190, 0x2000, v190
	global_load_dwordx2 v[208:209], v190, s[48:49] offset:-4096
	global_load_dwordx2 v[210:211], v190, s[48:49]
	v_add_u32_e32 v190, 0x2000, v190
	global_load_dwordx2 v[212:213], v190, s[48:49] offset:-4096
	global_load_dwordx2 v[214:215], v190, s[48:49]
	v_add_u32_e32 v190, 0x2000, v190
	global_load_dwordx2 v[216:217], v190, s[48:49] offset:-4096
	global_load_dwordx2 v[218:219], v190, s[48:49]
	v_add_u32_e32 v190, 0x2000, v190
	global_load_dwordx2 v[220:221], v190, s[48:49] offset:-4096
	global_load_dwordx2 v[222:223], v190, s[48:49]
	v_add_u32_e32 v190, 0x2000, v190
	global_load_dwordx2 v[224:225], v190, s[48:49] offset:-4096
	global_load_dwordx2 v[226:227], v190, s[48:49]
	v_mov_b32_e32 v17, v165
	s_nop 0
	v_pk_mul_f32 v[66:67], v[18:19], v[50:51] op_sel:[1,1] op_sel_hi:[1,0] neg_lo:[1,0]
	s_nop 0
	v_pk_fma_f32 v[18:19], v[18:19], v[50:51], v[66:67] op_sel_hi:[0,1,1]
	v_mov_b32_e32 v50, v166
	v_mov_b32_e32 v17, v167
	v_mov_b32_e32 v66, v168
	v_mov_b32_e32 v17, v169
	s_nop 0
	v_pk_mul_f32 v[40:41], v[22:23], v[68:69] op_sel:[1,0] op_sel_hi:[0,0] neg_lo:[1,0]
	v_mov_b32_e32 v17, v171
	v_pk_fma_f32 v[22:23], v[22:23], v[50:51], v[40:41] op_sel_hi:[1,0,1]
	v_pk_add_f32 v[40:41], v[24:25], v[42:43]
	v_pk_add_f32 v[24:25], v[24:25], v[42:43] neg_lo:[0,1] neg_hi:[0,1]
	s_nop 0
	v_pk_mul_f32 v[42:43], v[24:25], v[66:67] op_sel:[1,0] op_sel_hi:[0,0] neg_lo:[1,0]
	v_mov_b32_e32 v17, v172
	v_pk_fma_f32 v[24:25], v[24:25], v[66:67], v[42:43] op_sel_hi:[1,0,1]
	v_pk_add_f32 v[42:43], v[26:27], v[46:47]
	v_pk_add_f32 v[26:27], v[26:27], v[46:47] neg_lo:[0,1] neg_hi:[0,1]
	s_nop 0
	v_pk_mul_f32 v[46:47], v[26:27], v[68:69] op_sel_hi:[1,0]
	s_nop 0
	v_pk_fma_f32 v[26:27], v[26:27], v[50:51], v[46:47] op_sel:[1,0,0] op_sel_hi:[0,0,1] neg_lo:[1,0,0]
	v_pk_add_f32 v[46:47], v[28:29], v[44:45]
	v_pk_add_f32 v[28:29], v[28:29], v[44:45] neg_lo:[0,1] neg_hi:[0,1]
	v_mov_b32_e32 v17, v177
	v_xor_b32_e32 v44, 0x80000000, v29
	v_mov_b32_e32 v45, v28
	v_pk_add_f32 v[28:29], v[30:31], v[48:49]
	v_pk_add_f32 v[30:31], v[30:31], v[48:49] neg_lo:[0,1] neg_hi:[0,1]
	s_nop 0
	v_pk_mul_f32 v[48:49], v[30:31], v[68:69] op_sel_hi:[1,0] neg_lo:[0,1] neg_hi:[0,1]
	s_nop 0
	v_pk_fma_f32 v[30:31], v[30:31], v[50:51], v[48:49] op_sel:[1,0,0] op_sel_hi:[0,0,1] neg_lo:[1,0,0]
	v_pk_add_f32 v[48:49], v[32:33], v[38:39]
	v_pk_add_f32 v[32:33], v[32:33], v[38:39] neg_lo:[0,1] neg_hi:[0,1]
	s_nop 0
	v_pk_mul_f32 v[38:39], v[32:33], v[66:67] op_sel:[1,0] op_sel_hi:[0,0] neg_lo:[1,0]
	s_nop 0
	v_pk_fma_f32 v[32:33], v[32:33], v[66:67], v[38:39] op_sel_hi:[1,0,1] neg_lo:[0,1,0] neg_hi:[0,1,0]
	v_pk_add_f32 v[38:39], v[34:35], v[18:19]
	v_pk_add_f32 v[18:19], v[34:35], v[18:19] neg_lo:[0,1] neg_hi:[0,1]
	s_nop 0
	v_pk_mul_f32 v[34:35], v[18:19], v[68:69] op_sel:[1,0] op_sel_hi:[0,0] neg_lo:[1,0]
	v_mov_b32_e32 v68, v170
	v_pk_fma_f32 v[18:19], v[18:19], v[50:51], v[34:35] op_sel_hi:[1,0,1] neg_lo:[0,1,0] neg_hi:[0,1,0]
	v_pk_add_f32 v[50:51], v[36:37], v[28:29]
	v_pk_add_f32 v[28:29], v[36:37], v[28:29] neg_lo:[0,1] neg_hi:[0,1]
	v_pk_add_f32 v[34:35], v[70:71], v[46:47]
	v_pk_mul_f32 v[36:37], v[28:29], v[66:67] op_sel:[1,0] op_sel_hi:[0,0] neg_lo:[1,0]
	v_pk_add_f32 v[46:47], v[70:71], v[46:47] neg_lo:[0,1] neg_hi:[0,1]
	v_pk_fma_f32 v[28:29], v[28:29], v[66:67], v[36:37] op_sel_hi:[1,0,1]
	v_pk_add_f32 v[36:37], v[40:41], v[48:49]
	v_pk_add_f32 v[40:41], v[40:41], v[48:49] neg_lo:[0,1] neg_hi:[0,1]
	s_nop 0
	v_xor_b32_e32 v48, 0x80000000, v41
	v_mov_b32_e32 v49, v40
	v_pk_add_f32 v[40:41], v[42:43], v[38:39]
	v_pk_add_f32 v[38:39], v[42:43], v[38:39] neg_lo:[0,1] neg_hi:[0,1]
	s_nop 0
	v_pk_mul_f32 v[42:43], v[66:67], v[38:39] op_sel:[0,1] op_sel_hi:[0,0] neg_lo:[0,1]
	v_pk_fma_f32 v[38:39], v[38:39], v[66:67], v[42:43] op_sel_hi:[1,0,1] neg_lo:[0,1,0] neg_hi:[0,1,0]
	v_pk_add_f32 v[42:43], v[34:35], v[36:37]
	v_pk_add_f32 v[34:35], v[34:35], v[36:37] neg_lo:[0,1] neg_hi:[0,1]
	v_pk_add_f32 v[36:37], v[50:51], v[40:41]
	v_pk_add_f32 v[40:41], v[50:51], v[40:41] neg_lo:[0,1] neg_hi:[0,1]
	s_nop 0
	v_xor_b32_e32 v50, 0x80000000, v41
	v_mov_b32_e32 v51, v40
	v_pk_add_f32 v[40:41], v[42:43], v[36:37]
	v_pk_add_f32 v[36:37], v[42:43], v[36:37] neg_lo:[0,1] neg_hi:[0,1]
	v_pk_add_f32 v[42:43], v[34:35], v[50:51]
	v_pk_add_f32 v[34:35], v[34:35], v[50:51] neg_lo:[0,1] neg_hi:[0,1]
	v_pk_add_f32 v[50:51], v[46:47], v[48:49]
	v_pk_add_f32 v[46:47], v[46:47], v[48:49] neg_lo:[0,1] neg_hi:[0,1]
	v_pk_add_f32 v[48:49], v[28:29], v[38:39]
	v_pk_add_f32 v[28:29], v[28:29], v[38:39] neg_lo:[0,1] neg_hi:[0,1]
	s_nop 0
	v_xor_b32_e32 v38, 0x80000000, v29
	v_mov_b32_e32 v39, v28
	v_pk_add_f32 v[28:29], v[50:51], v[48:49]
	v_pk_add_f32 v[48:49], v[50:51], v[48:49] neg_lo:[0,1] neg_hi:[0,1]
	v_pk_add_f32 v[50:51], v[46:47], v[38:39]
	v_pk_add_f32 v[38:39], v[46:47], v[38:39] neg_lo:[0,1] neg_hi:[0,1]
	v_pk_add_f32 v[46:47], v[20:21], v[44:45]
	v_pk_add_f32 v[20:21], v[20:21], v[44:45] neg_lo:[0,1] neg_hi:[0,1]
	v_pk_add_f32 v[44:45], v[22:23], v[30:31]
	v_pk_add_f32 v[22:23], v[22:23], v[30:31] neg_lo:[0,1] neg_hi:[0,1]
	s_nop 0
	v_pk_mul_f32 v[30:31], v[66:67], v[22:23] op_sel:[0,1] op_sel_hi:[0,0] neg_lo:[0,1]
	v_pk_fma_f32 v[22:23], v[66:67], v[22:23], v[30:31] op_sel_hi:[0,1,1]
	v_pk_add_f32 v[30:31], v[24:25], v[32:33]
	v_pk_add_f32 v[24:25], v[24:25], v[32:33] neg_lo:[0,1] neg_hi:[0,1]
	s_nop 0
	v_xor_b32_e32 v32, 0x80000000, v25
	v_mov_b32_e32 v33, v24
	v_pk_add_f32 v[24:25], v[26:27], v[18:19]
	v_pk_add_f32 v[18:19], v[26:27], v[18:19] neg_lo:[0,1] neg_hi:[0,1]
	s_nop 0
	v_pk_mul_f32 v[26:27], v[66:67], v[18:19] op_sel:[0,1] op_sel_hi:[0,0] neg_lo:[0,1]
	v_pk_fma_f32 v[18:19], v[66:67], v[18:19], v[26:27] op_sel_hi:[0,1,1] neg_lo:[1,0,0] neg_hi:[1,0,0]
	v_pk_add_f32 v[26:27], v[46:47], v[30:31]
	v_pk_add_f32 v[30:31], v[46:47], v[30:31] neg_lo:[0,1] neg_hi:[0,1]
	v_pk_add_f32 v[46:47], v[44:45], v[24:25]
	v_pk_add_f32 v[24:25], v[44:45], v[24:25] neg_lo:[0,1] neg_hi:[0,1]
	v_mov_b32_e32 v66, v168
	v_xor_b32_e32 v44, 0x80000000, v25
	v_mov_b32_e32 v45, v24
	v_pk_add_f32 v[24:25], v[26:27], v[46:47]
	v_pk_add_f32 v[26:27], v[26:27], v[46:47] neg_lo:[0,1] neg_hi:[0,1]
	v_pk_add_f32 v[46:47], v[30:31], v[44:45]
	v_pk_add_f32 v[30:31], v[30:31], v[44:45] neg_lo:[0,1] neg_hi:[0,1]
	v_pk_add_f32 v[44:45], v[20:21], v[32:33]
	v_pk_add_f32 v[20:21], v[20:21], v[32:33] neg_lo:[0,1] neg_hi:[0,1]
	v_pk_add_f32 v[32:33], v[22:23], v[18:19]
	v_pk_add_f32 v[18:19], v[22:23], v[18:19] neg_lo:[0,1] neg_hi:[0,1]
	s_nop 0
	v_xor_b32_e32 v22, 0x80000000, v19
	v_mov_b32_e32 v23, v18
	v_pk_add_f32 v[18:19], v[44:45], v[32:33]
	v_pk_add_f32 v[32:33], v[44:45], v[32:33] neg_lo:[0,1] neg_hi:[0,1]
	v_pk_add_f32 v[44:45], v[20:21], v[22:23]
	v_pk_add_f32 v[20:21], v[20:21], v[22:23] neg_lo:[0,1] neg_hi:[0,1]
	ds_write_b64 v10, v[40:41]
	ds_write_b64 v13, v[24:25]
	ds_write_b64 v15, v[28:29]
	ds_write_b64 v52, v[18:19]
	ds_write_b64 v53, v[42:43]
	ds_write_b64 v54, v[46:47]
	ds_write_b64 v55, v[50:51]
	ds_write_b64 v56, v[44:45]
	ds_write_b64 v57, v[36:37]
	ds_write_b64 v58, v[26:27]
	ds_write_b64 v59, v[48:49]
	ds_write_b64 v60, v[32:33]
	ds_write_b64 v61, v[34:35]
	ds_write_b64 v62, v[30:31]
	ds_write_b64 v63, v[38:39]
	ds_write_b64 v64, v[20:21]
	v_mov_b32_e32 v10, v179
	v_mov_b32_e32 v64, v166
	v_lshlrev_b32_e32 v13, 3, v17
	v_lshlrev_b32_e32 v48, 3, v10
	v_add3_u32 v10, 0, v13, v48
	v_xor_b32_e32 v13, 1, v17
	v_xor_b32_e32 v34, 8, v17
	v_xor_b32_e32 v36, 9, v17
	v_lshlrev_b32_e32 v13, 3, v13
	v_xor_b32_e32 v15, 2, v17
	v_xor_b32_e32 v24, 3, v17
	v_xor_b32_e32 v26, 4, v17
	v_xor_b32_e32 v28, 5, v17
	v_xor_b32_e32 v30, 6, v17
	v_xor_b32_e32 v32, 7, v17
	v_lshlrev_b32_e32 v34, 3, v34
	v_lshlrev_b32_e32 v36, 3, v36
	v_xor_b32_e32 v38, 10, v17
	v_xor_b32_e32 v40, 11, v17
	v_xor_b32_e32 v42, 12, v17
	v_xor_b32_e32 v44, 13, v17
	v_xor_b32_e32 v46, 14, v17
	v_xor_b32_e32 v17, 15, v17
	v_add3_u32 v13, 0, v13, v48
	v_lshlrev_b32_e32 v15, 3, v15
	v_lshlrev_b32_e32 v24, 3, v24
	v_lshlrev_b32_e32 v26, 3, v26
	v_lshlrev_b32_e32 v28, 3, v28
	v_lshlrev_b32_e32 v30, 3, v30
	v_lshlrev_b32_e32 v32, 3, v32
	v_add3_u32 v55, 0, v34, v48
	v_add3_u32 v56, 0, v36, v48
	v_lshlrev_b32_e32 v38, 3, v38
	v_lshlrev_b32_e32 v40, 3, v40
	v_lshlrev_b32_e32 v42, 3, v42
	v_lshlrev_b32_e32 v44, 3, v44
	v_lshlrev_b32_e32 v46, 3, v46
	v_lshlrev_b32_e32 v17, 3, v17
	ds_read_b64 v[18:19], v10
	ds_read_b64 v[20:21], v13
	v_add3_u32 v15, 0, v15, v48
	v_add3_u32 v50, 0, v24, v48
	v_add3_u32 v51, 0, v26, v48
	v_add3_u32 v52, 0, v28, v48
	v_add3_u32 v53, 0, v30, v48
	v_add3_u32 v54, 0, v32, v48
	ds_read_b64 v[34:35], v55
	ds_read_b64 v[36:37], v56
	v_add3_u32 v57, 0, v38, v48
	v_add3_u32 v58, 0, v40, v48
	v_add3_u32 v59, 0, v42, v48
	v_add3_u32 v60, 0, v44, v48
	v_add3_u32 v61, 0, v46, v48
	v_add3_u32 v62, 0, v17, v48
	v_mov_b32_e32 v17, v164
	ds_read_b64 v[22:23], v15
	ds_read_b64 v[24:25], v50
	ds_read_b64 v[26:27], v51
	ds_read_b64 v[28:29], v52
	ds_read_b64 v[30:31], v53
	ds_read_b64 v[32:33], v54
	ds_read_b64 v[38:39], v57
	ds_read_b64 v[40:41], v58
	ds_read_b64 v[42:43], v59
	ds_read_b64 v[44:45], v60
	ds_read_b64 v[46:47], v61
	ds_read_b64 v[48:49], v62
	s_waitcnt lgkmcnt(13)
	v_pk_add_f32 v[70:71], v[18:19], v[34:35]
	v_mov_b32_e32 v17, v165
	v_pk_add_f32 v[18:19], v[18:19], v[34:35] neg_lo:[0,1] neg_hi:[0,1]
	v_mov_b32_e32 v17, v167
	s_waitcnt lgkmcnt(12)
	v_pk_add_f32 v[34:35], v[20:21], v[36:37]
	v_pk_add_f32 v[20:21], v[20:21], v[36:37] neg_lo:[0,1] neg_hi:[0,1]
	v_mov_b32_e32 v17, v169
	s_nop 0
	v_pk_mul_f32 v[36:37], v[20:21], v[68:69] op_sel:[1,0] op_sel_hi:[0,0] neg_lo:[1,1] neg_hi:[0,1]
	v_mov_b32_e32 v17, v171
	v_pk_fma_f32 v[20:21], v[20:21], v[64:65], v[36:37] op_sel_hi:[1,0,1]
	s_waitcnt lgkmcnt(5)
	v_pk_add_f32 v[36:37], v[22:23], v[38:39]
	v_pk_add_f32 v[22:23], v[22:23], v[38:39] neg_lo:[0,1] neg_hi:[0,1]
	s_nop 0
	v_pk_mul_f32 v[38:39], v[22:23], v[66:67] op_sel:[1,0] op_sel_hi:[0,0] neg_lo:[1,1] neg_hi:[0,1]
	v_mov_b32_e32 v17, v172
	v_pk_fma_f32 v[22:23], v[22:23], v[66:67], v[38:39] op_sel_hi:[1,0,1]
	s_waitcnt lgkmcnt(4)
	v_pk_add_f32 v[38:39], v[24:25], v[40:41]
	v_pk_add_f32 v[24:25], v[24:25], v[40:41] neg_lo:[0,1] neg_hi:[0,1]
	s_nop 0
	v_pk_mul_f32 v[40:41], v[24:25], v[68:69] op_sel_hi:[1,0]
	s_nop 0
	v_pk_fma_f32 v[24:25], v[24:25], v[64:65], v[40:41] op_sel:[1,0,0] op_sel_hi:[0,0,1] neg_lo:[1,1,0] neg_hi:[0,1,0]
	s_waitcnt lgkmcnt(3)
	v_pk_add_f32 v[40:41], v[26:27], v[42:43]
	v_pk_add_f32 v[26:27], v[26:27], v[42:43] neg_lo:[0,1] neg_hi:[0,1]
	s_nop 0
	v_xor_b32_e32 v73, 0x80000000, v26
	v_mov_b32_e32 v72, v27
	s_waitcnt lgkmcnt(2)
	v_pk_add_f32 v[26:27], v[28:29], v[44:45]
	v_pk_add_f32 v[28:29], v[28:29], v[44:45] neg_lo:[0,1] neg_hi:[0,1]
	s_nop 0
	v_pk_mul_f32 v[42:43], v[28:29], v[68:69] op_sel_hi:[1,0] neg_lo:[0,1] neg_hi:[0,1]
	s_nop 0
	v_pk_fma_f32 v[28:29], v[28:29], v[64:65], v[42:43] op_sel:[1,0,0] op_sel_hi:[0,0,1] neg_lo:[1,1,0] neg_hi:[0,1,0]
	s_waitcnt lgkmcnt(1)
	v_pk_add_f32 v[42:43], v[30:31], v[46:47]
	v_pk_add_f32 v[30:31], v[30:31], v[46:47] neg_lo:[0,1] neg_hi:[0,1]
	s_nop 0
	v_pk_mul_f32 v[44:45], v[30:31], v[66:67] op_sel:[1,0] op_sel_hi:[0,0] neg_lo:[1,1] neg_hi:[0,1]
	s_nop 0
	v_pk_fma_f32 v[30:31], v[30:31], v[66:67], v[44:45] op_sel_hi:[1,0,1] neg_lo:[0,1,0] neg_hi:[0,1,0]
	s_waitcnt lgkmcnt(0)
	v_pk_add_f32 v[44:45], v[32:33], v[48:49]
	v_pk_add_f32 v[32:33], v[32:33], v[48:49] neg_lo:[0,1] neg_hi:[0,1]
	v_pk_add_f32 v[48:49], v[34:35], v[26:27]
	v_pk_add_f32 v[26:27], v[34:35], v[26:27] neg_lo:[0,1] neg_hi:[0,1]
	s_nop 0
	v_pk_mul_f32 v[34:35], v[26:27], v[66:67] op_sel:[1,0] op_sel_hi:[0,0] neg_lo:[1,1] neg_hi:[0,1]
	v_pk_fma_f32 v[26:27], v[26:27], v[66:67], v[34:35] op_sel_hi:[1,0,1]
	v_pk_add_f32 v[34:35], v[36:37], v[42:43]
	v_pk_add_f32 v[36:37], v[36:37], v[42:43] neg_lo:[0,1] neg_hi:[0,1]
	v_pk_mul_f32 v[46:47], v[32:33], v[68:69] op_sel:[1,0] op_sel_hi:[0,0] neg_lo:[1,1] neg_hi:[0,1]
	v_xor_b32_e32 v43, 0x80000000, v36
	v_mov_b32_e32 v42, v37
	v_pk_add_f32 v[36:37], v[38:39], v[44:45]
	v_pk_add_f32 v[38:39], v[38:39], v[44:45] neg_lo:[0,1] neg_hi:[0,1]
	v_pk_fma_f32 v[46:47], v[32:33], v[64:65], v[46:47] op_sel_hi:[1,0,1] neg_lo:[0,1,0] neg_hi:[0,1,0]
	v_pk_add_f32 v[32:33], v[70:71], v[40:41]
	v_pk_mul_f32 v[44:45], v[38:39], v[66:67] op_sel:[1,0] op_sel_hi:[0,0] neg_lo:[1,1] neg_hi:[0,1]
	v_pk_add_f32 v[40:41], v[70:71], v[40:41] neg_lo:[0,1] neg_hi:[0,1]
	v_pk_fma_f32 v[38:39], v[38:39], v[66:67], v[44:45] op_sel_hi:[1,0,1] neg_lo:[0,1,0] neg_hi:[0,1,0]
	v_pk_add_f32 v[44:45], v[32:33], v[34:35]
	v_pk_add_f32 v[32:33], v[32:33], v[34:35] neg_lo:[0,1] neg_hi:[0,1]
	v_pk_add_f32 v[34:35], v[48:49], v[36:37]
	v_pk_add_f32 v[36:37], v[48:49], v[36:37] neg_lo:[0,1] neg_hi:[0,1]
	v_pk_add_f32 v[64:65], v[44:45], v[34:35]
	v_xor_b32_e32 v49, 0x80000000, v36
	v_mov_b32_e32 v48, v37
	v_pk_add_f32 v[36:37], v[44:45], v[34:35] neg_lo:[0,1] neg_hi:[0,1]
	v_pk_add_f32 v[68:69], v[32:33], v[48:49]
	v_pk_add_f32 v[44:45], v[32:33], v[48:49] neg_lo:[0,1] neg_hi:[0,1]
	v_pk_add_f32 v[32:33], v[40:41], v[42:43]
	v_pk_add_f32 v[34:35], v[40:41], v[42:43] neg_lo:[0,1] neg_hi:[0,1]
	v_pk_add_f32 v[40:41], v[26:27], v[38:39]
	v_pk_add_f32 v[26:27], v[26:27], v[38:39] neg_lo:[0,1] neg_hi:[0,1]
	v_pk_add_f32 v[42:43], v[32:33], v[40:41] neg_lo:[0,1] neg_hi:[0,1]
	v_xor_b32_e32 v39, 0x80000000, v26
	v_mov_b32_e32 v38, v27
	v_pk_add_f32 v[26:27], v[32:33], v[40:41]
	v_pk_add_f32 v[40:41], v[20:21], v[28:29]
	v_pk_add_f32 v[20:21], v[20:21], v[28:29] neg_lo:[0,1] neg_hi:[0,1]
	v_pk_add_f32 v[32:33], v[34:35], v[38:39]
	v_pk_mul_f32 v[28:29], v[66:67], v[20:21] op_sel:[0,1] op_sel_hi:[0,0] neg_lo:[1,1] neg_hi:[1,0]
	v_pk_fma_f32 v[20:21], v[66:67], v[20:21], v[28:29] op_sel_hi:[0,1,1]
	v_pk_add_f32 v[28:29], v[22:23], v[30:31]
	v_pk_add_f32 v[22:23], v[22:23], v[30:31] neg_lo:[0,1] neg_hi:[0,1]
	v_pk_add_f32 v[38:39], v[34:35], v[38:39] neg_lo:[0,1] neg_hi:[0,1]
	v_xor_b32_e32 v31, 0x80000000, v22
	v_mov_b32_e32 v30, v23
	v_pk_add_f32 v[22:23], v[24:25], v[46:47]
	v_pk_add_f32 v[24:25], v[24:25], v[46:47] neg_lo:[0,1] neg_hi:[0,1]
	v_pk_add_f32 v[34:35], v[18:19], v[72:73]
	v_pk_mul_f32 v[46:47], v[66:67], v[24:25] op_sel:[0,1] op_sel_hi:[0,0] neg_lo:[1,1] neg_hi:[1,0]
	v_pk_fma_f32 v[24:25], v[66:67], v[24:25], v[46:47] op_sel_hi:[0,1,1] neg_lo:[1,0,0] neg_hi:[1,0,0]
	v_pk_add_f32 v[46:47], v[34:35], v[28:29]
	v_pk_add_f32 v[28:29], v[34:35], v[28:29] neg_lo:[0,1] neg_hi:[0,1]
	v_pk_add_f32 v[34:35], v[40:41], v[22:23]
	v_pk_add_f32 v[22:23], v[40:41], v[22:23] neg_lo:[0,1] neg_hi:[0,1]
	v_pk_add_f32 v[18:19], v[18:19], v[72:73] neg_lo:[0,1] neg_hi:[0,1]
	v_pk_add_f32 v[66:67], v[28:29], v[22:23] op_sel:[0,1] op_sel_hi:[1,0] neg_hi:[0,1]
	v_pk_add_f32 v[48:49], v[28:29], v[22:23] op_sel:[0,1] op_sel_hi:[1,0] neg_lo:[0,1]
	v_pk_add_f32 v[28:29], v[18:19], v[30:31]
	v_pk_add_f32 v[18:19], v[18:19], v[30:31] neg_lo:[0,1] neg_hi:[0,1]
	v_pk_add_f32 v[30:31], v[20:21], v[24:25]
	v_pk_add_f32 v[20:21], v[20:21], v[24:25] neg_lo:[0,1] neg_hi:[0,1]
	v_pk_add_f32 v[22:23], v[46:47], v[34:35]
	v_xor_b32_e32 v25, 0x80000000, v20
	v_add_u32_e32 v20, 0x2000, v16
	v_mov_b32_e32 v24, v21
	v_ashrrev_i32_e32 v21, 31, v20
	v_lshl_add_u64 v[20:21], v[20:21], 3, s[48:49]
	s_waitcnt vmcnt(0)
	v_pk_add_f32 v[40:41], v[46:47], v[34:35] neg_lo:[0,1] neg_hi:[0,1]
	v_pk_add_f32 v[34:35], v[18:19], v[24:25]
	v_pk_add_f32 v[18:19], v[18:19], v[24:25] neg_lo:[0,1] neg_hi:[0,1]
	v_pk_add_f32 v[70:71], v[28:29], v[30:31]
	v_pk_add_f32 v[46:47], v[28:29], v[30:31] neg_lo:[0,1] neg_hi:[0,1]
	s_nop 0
	v_pk_mul_f32 v[24:25], v[64:65], v[196:197] op_sel:[1,1] op_sel_hi:[1,0] neg_lo:[1,0]
	s_nop 0
	v_pk_fma_f32 v[20:21], v[64:65], v[196:197], v[24:25] op_sel_hi:[0,1,1]
	v_add_u32_e32 v24, 0x2200, v16
	v_ashrrev_i32_e32 v25, 31, v24
	v_lshl_add_u64 v[24:25], v[24:25], 3, s[48:49]
	s_nop 0
	v_pk_mul_f32 v[28:29], v[198:199], v[22:23] op_sel:[1,1] op_sel_hi:[0,1] neg_lo:[0,1]
	v_pk_fma_f32 v[22:23], v[198:199], v[22:23], v[28:29] op_sel_hi:[1,0,1]
	v_add_u32_e32 v24, 0x2400, v16
	v_ashrrev_i32_e32 v25, 31, v24
	v_lshl_add_u64 v[24:25], v[24:25], 3, s[48:49]
	s_nop 0
	v_pk_mul_f32 v[28:29], v[26:27], v[200:201] op_sel:[1,1] op_sel_hi:[1,0] neg_lo:[1,0]
	s_nop 0
	v_pk_fma_f32 v[24:25], v[26:27], v[200:201], v[28:29] op_sel_hi:[0,1,1]
	v_add_u32_e32 v26, 0x2600, v16
	v_ashrrev_i32_e32 v27, 31, v26
	v_lshl_add_u64 v[26:27], v[26:27], 3, s[48:49]
	s_nop 0
	v_pk_mul_f32 v[28:29], v[202:203], v[70:71] op_sel:[1,1] op_sel_hi:[0,1] neg_lo:[0,1]
	v_pk_fma_f32 v[26:27], v[202:203], v[70:71], v[28:29] op_sel_hi:[1,0,1]
	v_add_u32_e32 v28, 0x2800, v16
	v_ashrrev_i32_e32 v29, 31, v28
	v_lshl_add_u64 v[28:29], v[28:29], 3, s[48:49]
	s_nop 0
	v_pk_mul_f32 v[30:31], v[68:69], v[204:205] op_sel:[1,1] op_sel_hi:[1,0] neg_lo:[1,0]
	s_nop 0
	v_pk_fma_f32 v[28:29], v[68:69], v[204:205], v[30:31] op_sel_hi:[0,1,1]
	v_add_u32_e32 v30, 0x2a00, v16
	v_ashrrev_i32_e32 v31, 31, v30
	v_lshl_add_u64 v[30:31], v[30:31], 3, s[48:49]
	s_nop 0
	v_pk_mul_f32 v[64:65], v[206:207], v[66:67] op_sel:[1,1] op_sel_hi:[0,1] neg_lo:[0,1]
	v_pk_fma_f32 v[30:31], v[206:207], v[66:67], v[64:65] op_sel_hi:[1,0,1]
	v_add_u32_e32 v64, 0x2c00, v16
	v_ashrrev_i32_e32 v65, 31, v64
	v_lshl_add_u64 v[64:65], v[64:65], 3, s[48:49]
	s_nop 0
	v_pk_mul_f32 v[66:67], v[32:33], v[208:209] op_sel:[1,1] op_sel_hi:[1,0] neg_lo:[1,0]
	s_nop 0
	v_pk_fma_f32 v[32:33], v[32:33], v[208:209], v[66:67] op_sel_hi:[0,1,1]
	v_add_u32_e32 v64, 0x2e00, v16
	v_ashrrev_i32_e32 v65, 31, v64
	v_lshl_add_u64 v[64:65], v[64:65], 3, s[48:49]
	s_nop 0
	v_pk_mul_f32 v[66:67], v[210:211], v[34:35] op_sel:[1,1] op_sel_hi:[0,1] neg_lo:[0,1]
	v_pk_fma_f32 v[34:35], v[210:211], v[34:35], v[66:67] op_sel_hi:[1,0,1]
	v_add_u32_e32 v64, 0x3000, v16
	v_ashrrev_i32_e32 v65, 31, v64
	v_lshl_add_u64 v[64:65], v[64:65], 3, s[48:49]
	s_nop 0
	v_pk_mul_f32 v[66:67], v[36:37], v[212:213] op_sel:[1,1] op_sel_hi:[1,0] neg_lo:[1,0]
	s_nop 0
	v_pk_fma_f32 v[36:37], v[36:37], v[212:213], v[66:67] op_sel_hi:[0,1,1]
	v_add_u32_e32 v64, 0x3200, v16
	v_ashrrev_i32_e32 v65, 31, v64
	v_lshl_add_u64 v[64:65], v[64:65], 3, s[48:49]
	v_pk_add_f32 v[68:69], v[20:21], v[36:37]
	v_pk_add_f32 v[20:21], v[20:21], v[36:37] neg_lo:[0,1] neg_hi:[0,1]
	s_nop 0
	v_pk_mul_f32 v[66:67], v[40:41], v[214:215] op_sel:[1,1] op_sel_hi:[1,0] neg_lo:[1,0]
	s_nop 0
	v_pk_fma_f32 v[40:41], v[40:41], v[214:215], v[66:67] op_sel_hi:[0,1,1]
	v_add_u32_e32 v64, 0x3400, v16
	v_ashrrev_i32_e32 v65, 31, v64
	v_lshl_add_u64 v[64:65], v[64:65], 3, s[48:49]
	v_pk_add_f32 v[36:37], v[22:23], v[40:41]
	v_pk_add_f32 v[22:23], v[22:23], v[40:41] neg_lo:[0,1] neg_hi:[0,1]
	s_nop 0
	v_pk_mul_f32 v[66:67], v[42:43], v[216:217] op_sel:[1,1] op_sel_hi:[1,0] neg_lo:[1,0]
	s_nop 0
	v_pk_fma_f32 v[42:43], v[42:43], v[216:217], v[66:67] op_sel_hi:[0,1,1]
	v_add_u32_e32 v64, 0x3600, v16
	v_ashrrev_i32_e32 v65, 31, v64
	v_lshl_add_u64 v[64:65], v[64:65], 3, s[48:49]
	s_nop 0
	v_pk_mul_f32 v[66:67], v[46:47], v[218:219] op_sel:[1,1] op_sel_hi:[1,0] neg_lo:[1,0]
	s_nop 0
	v_pk_fma_f32 v[46:47], v[46:47], v[218:219], v[66:67] op_sel_hi:[0,1,1]
	v_add_u32_e32 v64, 0x3800, v16
	v_ashrrev_i32_e32 v65, 31, v64
	v_lshl_add_u64 v[64:65], v[64:65], 3, s[48:49]
	s_nop 0
	v_pk_mul_f32 v[66:67], v[44:45], v[220:221] op_sel:[1,1] op_sel_hi:[1,0] neg_lo:[1,0]
	s_nop 0
	v_pk_fma_f32 v[44:45], v[44:45], v[220:221], v[66:67] op_sel_hi:[0,1,1]
	v_add_u32_e32 v64, 0x3a00, v16
	v_ashrrev_i32_e32 v65, 31, v64
	v_lshl_add_u64 v[64:65], v[64:65], 3, s[48:49]
	s_nop 0
	v_pk_mul_f32 v[66:67], v[48:49], v[222:223] op_sel:[1,1] op_sel_hi:[1,0] neg_lo:[1,0]
	s_nop 0
	v_pk_fma_f32 v[48:49], v[48:49], v[222:223], v[66:67] op_sel_hi:[0,1,1]
	v_add_u32_e32 v64, 0x3c00, v16
	v_ashrrev_i32_e32 v65, 31, v64
	v_lshl_add_u64 v[64:65], v[64:65], 3, s[48:49]
	v_add_u32_e32 v16, 0x3e00, v16
	v_ashrrev_i32_e32 v17, 31, v16
	v_lshl_add_u64 v[16:17], v[16:17], 3, s[48:49]
	s_nop 0
	v_pk_mul_f32 v[66:67], v[38:39], v[224:225] op_sel:[1,1] op_sel_hi:[1,0] neg_lo:[1,0]
	s_nop 0
	v_pk_fma_f32 v[38:39], v[38:39], v[224:225], v[66:67] op_sel_hi:[0,1,1]
	s_nop 0
	v_pk_mul_f32 v[64:65], v[18:19], v[226:227] op_sel:[1,1] op_sel_hi:[1,0] neg_lo:[1,0]
	v_mov_b32_e32 v66, v170
	v_pk_fma_f32 v[16:17], v[18:19], v[226:227], v[64:65] op_sel_hi:[0,1,1]
	v_mov_b32_e32 v18, v164
	v_mov_b32_e32 v19, v167
	v_mov_b32_e32 v18, v165
	v_mov_b32_e32 v64, v168
	v_mov_b32_e32 v18, v166
	s_nop 0
	v_mov_b32_e32 v19, v169
	s_nop 0
	v_mov_b32_e32 v19, v171
	v_pk_mul_f32 v[40:41], v[22:23], v[66:67] op_sel:[1,0] op_sel_hi:[0,0] neg_lo:[1,0]
	v_mov_b32_e32 v19, v172
	s_nop 0
	v_pk_fma_f32 v[22:23], v[22:23], v[18:19], v[40:41] op_sel_hi:[1,0,1]
	v_pk_add_f32 v[40:41], v[24:25], v[42:43]
	v_pk_add_f32 v[24:25], v[24:25], v[42:43] neg_lo:[0,1] neg_hi:[0,1]
	s_nop 0
	v_pk_mul_f32 v[42:43], v[24:25], v[64:65] op_sel:[1,0] op_sel_hi:[0,0] neg_lo:[1,0]
	s_nop 0
	v_pk_fma_f32 v[24:25], v[24:25], v[64:65], v[42:43] op_sel_hi:[1,0,1]
	v_pk_add_f32 v[42:43], v[26:27], v[46:47]
	v_pk_add_f32 v[26:27], v[26:27], v[46:47] neg_lo:[0,1] neg_hi:[0,1]
	s_nop 0
	v_pk_mul_f32 v[46:47], v[26:27], v[66:67] op_sel_hi:[1,0]
	s_nop 0
	v_pk_fma_f32 v[26:27], v[26:27], v[18:19], v[46:47] op_sel:[1,0,0] op_sel_hi:[0,0,1] neg_lo:[1,0,0]
	v_pk_add_f32 v[46:47], v[28:29], v[44:45]
	v_pk_add_f32 v[28:29], v[28:29], v[44:45] neg_lo:[0,1] neg_hi:[0,1]
	s_nop 0
	v_xor_b32_e32 v44, 0x80000000, v29
	v_mov_b32_e32 v45, v28
	v_pk_add_f32 v[28:29], v[30:31], v[48:49]
	v_pk_add_f32 v[30:31], v[30:31], v[48:49] neg_lo:[0,1] neg_hi:[0,1]
	s_nop 0
	v_pk_mul_f32 v[48:49], v[30:31], v[66:67] op_sel_hi:[1,0] neg_lo:[0,1] neg_hi:[0,1]
	s_nop 0
	v_pk_fma_f32 v[30:31], v[30:31], v[18:19], v[48:49] op_sel:[1,0,0] op_sel_hi:[0,0,1] neg_lo:[1,0,0]
	v_pk_add_f32 v[48:49], v[32:33], v[38:39]
	v_pk_add_f32 v[32:33], v[32:33], v[38:39] neg_lo:[0,1] neg_hi:[0,1]
	s_nop 0
	v_pk_mul_f32 v[38:39], v[32:33], v[64:65] op_sel:[1,0] op_sel_hi:[0,0] neg_lo:[1,0]
	s_nop 0
	v_pk_fma_f32 v[32:33], v[32:33], v[64:65], v[38:39] op_sel_hi:[1,0,1] neg_lo:[0,1,0] neg_hi:[0,1,0]
	v_pk_add_f32 v[38:39], v[34:35], v[16:17]
	v_pk_add_f32 v[16:17], v[34:35], v[16:17] neg_lo:[0,1] neg_hi:[0,1]
	s_nop 0
	v_pk_mul_f32 v[34:35], v[16:17], v[66:67] op_sel:[1,0] op_sel_hi:[0,0] neg_lo:[1,0]
	s_nop 0
	v_pk_fma_f32 v[16:17], v[16:17], v[18:19], v[34:35] op_sel_hi:[1,0,1] neg_lo:[0,1,0] neg_hi:[0,1,0]
	v_pk_add_f32 v[18:19], v[68:69], v[46:47]
	v_pk_add_f32 v[34:35], v[68:69], v[46:47] neg_lo:[0,1] neg_hi:[0,1]
	v_pk_add_f32 v[46:47], v[36:37], v[28:29]
	v_pk_add_f32 v[28:29], v[36:37], v[28:29] neg_lo:[0,1] neg_hi:[0,1]
	s_nop 0
	v_pk_mul_f32 v[36:37], v[28:29], v[64:65] op_sel:[1,0] op_sel_hi:[0,0] neg_lo:[1,0]
	s_nop 0
	v_pk_fma_f32 v[28:29], v[28:29], v[64:65], v[36:37] op_sel_hi:[1,0,1]
	v_pk_add_f32 v[36:37], v[40:41], v[48:49]
	v_pk_add_f32 v[40:41], v[40:41], v[48:49] neg_lo:[0,1] neg_hi:[0,1]
	s_nop 0
	v_xor_b32_e32 v48, 0x80000000, v41
	v_mov_b32_e32 v49, v40
	v_pk_add_f32 v[40:41], v[42:43], v[38:39]
	v_pk_add_f32 v[38:39], v[42:43], v[38:39] neg_lo:[0,1] neg_hi:[0,1]
	s_nop 0
	v_pk_mul_f32 v[42:43], v[64:65], v[38:39] op_sel:[0,1] op_sel_hi:[0,0] neg_lo:[0,1]
	v_pk_fma_f32 v[38:39], v[38:39], v[64:65], v[42:43] op_sel_hi:[1,0,1] neg_lo:[0,1,0] neg_hi:[0,1,0]
	v_pk_add_f32 v[42:43], v[18:19], v[36:37]
	v_pk_add_f32 v[18:19], v[18:19], v[36:37] neg_lo:[0,1] neg_hi:[0,1]
	v_pk_add_f32 v[36:37], v[46:47], v[40:41]
	v_pk_add_f32 v[40:41], v[46:47], v[40:41] neg_lo:[0,1] neg_hi:[0,1]
	s_nop 0
	v_xor_b32_e32 v46, 0x80000000, v41
	v_mov_b32_e32 v47, v40
	v_pk_add_f32 v[40:41], v[42:43], v[36:37]
	v_pk_add_f32 v[36:37], v[42:43], v[36:37] neg_lo:[0,1] neg_hi:[0,1]
	v_pk_add_f32 v[42:43], v[18:19], v[46:47]
	v_pk_add_f32 v[18:19], v[18:19], v[46:47] neg_lo:[0,1] neg_hi:[0,1]
	v_pk_add_f32 v[46:47], v[34:35], v[48:49]
	v_pk_add_f32 v[34:35], v[34:35], v[48:49] neg_lo:[0,1] neg_hi:[0,1]
	v_pk_add_f32 v[48:49], v[28:29], v[38:39]
	v_pk_add_f32 v[28:29], v[28:29], v[38:39] neg_lo:[0,1] neg_hi:[0,1]
	s_nop 0
	v_xor_b32_e32 v38, 0x80000000, v29
	v_mov_b32_e32 v39, v28
	v_pk_add_f32 v[28:29], v[46:47], v[48:49]
	v_pk_add_f32 v[46:47], v[46:47], v[48:49] neg_lo:[0,1] neg_hi:[0,1]
	v_pk_add_f32 v[48:49], v[34:35], v[38:39]
	v_pk_add_f32 v[34:35], v[34:35], v[38:39] neg_lo:[0,1] neg_hi:[0,1]
	v_pk_add_f32 v[38:39], v[20:21], v[44:45]
	v_pk_add_f32 v[20:21], v[20:21], v[44:45] neg_lo:[0,1] neg_hi:[0,1]
	v_pk_add_f32 v[44:45], v[22:23], v[30:31]
	v_pk_add_f32 v[22:23], v[22:23], v[30:31] neg_lo:[0,1] neg_hi:[0,1]
	s_nop 0
	v_pk_mul_f32 v[30:31], v[64:65], v[22:23] op_sel:[0,1] op_sel_hi:[0,0] neg_lo:[0,1]
	v_pk_fma_f32 v[22:23], v[64:65], v[22:23], v[30:31] op_sel_hi:[0,1,1]
	v_pk_add_f32 v[30:31], v[24:25], v[32:33]
	v_pk_add_f32 v[24:25], v[24:25], v[32:33] neg_lo:[0,1] neg_hi:[0,1]
	s_nop 0
	v_xor_b32_e32 v32, 0x80000000, v25
	v_mov_b32_e32 v33, v24
	v_pk_add_f32 v[24:25], v[26:27], v[16:17]
	v_pk_add_f32 v[16:17], v[26:27], v[16:17] neg_lo:[0,1] neg_hi:[0,1]
	s_nop 0
	v_pk_mul_f32 v[26:27], v[64:65], v[16:17] op_sel:[0,1] op_sel_hi:[0,0] neg_lo:[0,1]
	v_pk_fma_f32 v[16:17], v[64:65], v[16:17], v[26:27] op_sel_hi:[0,1,1] neg_lo:[1,0,0] neg_hi:[1,0,0]
	v_pk_add_f32 v[26:27], v[38:39], v[30:31]
	v_pk_add_f32 v[30:31], v[38:39], v[30:31] neg_lo:[0,1] neg_hi:[0,1]
	v_pk_add_f32 v[38:39], v[44:45], v[24:25]
	v_pk_add_f32 v[24:25], v[44:45], v[24:25] neg_lo:[0,1] neg_hi:[0,1]
	s_nop 0
	v_xor_b32_e32 v44, 0x80000000, v25
	v_mov_b32_e32 v45, v24
	v_pk_add_f32 v[24:25], v[26:27], v[38:39]
	v_pk_add_f32 v[26:27], v[26:27], v[38:39] neg_lo:[0,1] neg_hi:[0,1]
	v_pk_add_f32 v[38:39], v[30:31], v[44:45]
	v_pk_add_f32 v[30:31], v[30:31], v[44:45] neg_lo:[0,1] neg_hi:[0,1]
	v_pk_add_f32 v[44:45], v[20:21], v[32:33]
	v_pk_add_f32 v[20:21], v[20:21], v[32:33] neg_lo:[0,1] neg_hi:[0,1]
	v_pk_add_f32 v[32:33], v[22:23], v[16:17]
	v_pk_add_f32 v[16:17], v[22:23], v[16:17] neg_lo:[0,1] neg_hi:[0,1]
	s_nop 0
	v_xor_b32_e32 v22, 0x80000000, v17
	v_mov_b32_e32 v23, v16
	v_pk_add_f32 v[16:17], v[44:45], v[32:33]
	v_pk_add_f32 v[32:33], v[44:45], v[32:33] neg_lo:[0,1] neg_hi:[0,1]
	v_pk_add_f32 v[44:45], v[20:21], v[22:23]
	v_pk_add_f32 v[20:21], v[20:21], v[22:23] neg_lo:[0,1] neg_hi:[0,1]
	ds_write_b64 v10, v[40:41]
	ds_write_b64 v13, v[24:25]
	ds_write_b64 v15, v[28:29]
	ds_write_b64 v50, v[16:17]
	ds_write_b64 v51, v[42:43]
	ds_write_b64 v52, v[38:39]
	ds_write_b64 v53, v[48:49]
	ds_write_b64 v54, v[44:45]
	ds_write_b64 v55, v[36:37]
	ds_write_b64 v56, v[26:27]
	ds_write_b64 v57, v[46:47]
	ds_write_b64 v58, v[32:33]
	ds_write_b64 v59, v[18:19]
	ds_write_b64 v60, v[30:31]
	ds_write_b64 v61, v[34:35]
	ds_write_b64 v62, v[20:21]
	v_mov_b32_e32 v10, v176
	v_mov_b32_e32 v50, v173
	s_waitcnt lgkmcnt(0)
	s_barrier
	v_add_u32_e32 v13, v50, v10
	v_lshl_add_u32 v13, v13, 3, 0
	ds_read2_b64 v[16:19], v13 offset1:16
	v_xad_u32 v15, v50, 1, v10
	v_lshl_add_u32 v15, v15, 3, 0
	s_waitcnt lgkmcnt(0)
	v_pk_fma_f32 v[16:17], v[16:17], 0, v[16:17] op_sel:[1,0,0] op_sel_hi:[0,0,1] neg_hi:[1,0,0]
	v_pk_fma_f32 v[22:23], v[182:183], s[92:93], v[182:183] op_sel:[1,0,0] op_sel_hi:[0,1,1]
	v_pk_mul_f32 v[24:25], v[22:23], v[18:19] op_sel:[1,1] op_sel_hi:[1,0] neg_hi:[0,1]
	s_nop 0
	v_pk_fma_f32 v[18:19], v[18:19], v[22:23], v[24:25] op_sel_hi:[1,0,1]
	v_pk_mul_f32 v[24:25], v[182:183], v[22:23] op_sel:[1,1] op_sel_hi:[0,1] neg_lo:[0,1]
	v_pk_fma_f32 v[26:27], v[182:183], v[22:23], v[24:25] op_sel_hi:[1,0,1]
	ds_read2_b64 v[22:25], v15 offset0:32 offset1:48
	s_waitcnt lgkmcnt(0)
	v_pk_mul_f32 v[28:29], v[22:23], v[26:27] op_sel:[1,1] op_sel_hi:[0,1] neg_hi:[1,0]
	s_nop 0
	v_pk_fma_f32 v[22:23], v[22:23], v[26:27], v[28:29] op_sel_hi:[1,0,1]
	v_pk_mul_f32 v[28:29], v[182:183], v[26:27] op_sel:[1,1] op_sel_hi:[0,1] neg_lo:[0,1]
	v_pk_fma_f32 v[26:27], v[182:183], v[26:27], v[28:29] op_sel_hi:[1,0,1]
	s_nop 0
	v_pk_mul_f32 v[28:29], v[24:25], v[26:27] op_sel:[1,1] op_sel_hi:[0,1] neg_hi:[1,0]
	s_nop 0
	v_pk_fma_f32 v[24:25], v[24:25], v[26:27], v[28:29] op_sel_hi:[1,0,1]
	v_pk_mul_f32 v[28:29], v[182:183], v[26:27] op_sel:[1,1] op_sel_hi:[0,1] neg_lo:[0,1]
	v_pk_fma_f32 v[26:27], v[182:183], v[26:27], v[28:29] op_sel_hi:[1,0,1]
	v_xad_u32 v28, v50, 2, v10
	v_lshl_add_u32 v51, v28, 3, 0
	ds_read2_b64 v[28:31], v51 offset0:64 offset1:80
	v_pk_mul_f32 v[32:33], v[182:183], v[26:27] op_sel:[1,1] op_sel_hi:[0,1] neg_lo:[0,1]
	s_waitcnt lgkmcnt(0)
	v_pk_mul_f32 v[34:35], v[28:29], v[26:27] op_sel:[1,1] op_sel_hi:[0,1] neg_hi:[1,0]
	s_nop 0
	v_pk_fma_f32 v[28:29], v[28:29], v[26:27], v[34:35] op_sel_hi:[1,0,1]
	v_pk_fma_f32 v[34:35], v[182:183], v[26:27], v[32:33] op_sel_hi:[1,0,1]
	s_nop 0
	v_pk_mul_f32 v[26:27], v[30:31], v[34:35] op_sel:[1,1] op_sel_hi:[0,1] neg_hi:[1,0]
	v_pk_fma_f32 v[26:27], v[30:31], v[34:35], v[26:27] op_sel_hi:[1,0,1]
	v_xad_u32 v30, v50, 3, v10
	v_lshl_add_u32 v54, v30, 3, 0
	ds_read2_b64 v[30:33], v54 offset0:96 offset1:112
	v_pk_mul_f32 v[36:37], v[182:183], v[34:35] op_sel:[1,1] op_sel_hi:[0,1] neg_lo:[0,1]
	v_pk_fma_f32 v[34:35], v[182:183], v[34:35], v[36:37] op_sel_hi:[1,0,1]
	s_waitcnt lgkmcnt(0)
	v_pk_mul_f32 v[36:37], v[30:31], v[34:35] op_sel:[1,1] op_sel_hi:[0,1] neg_hi:[1,0]
	s_nop 0
	v_pk_fma_f32 v[30:31], v[30:31], v[34:35], v[36:37] op_sel_hi:[1,0,1]
	v_pk_mul_f32 v[36:37], v[182:183], v[34:35] op_sel:[1,1] op_sel_hi:[0,1] neg_lo:[0,1]
	v_pk_fma_f32 v[34:35], v[182:183], v[34:35], v[36:37] op_sel_hi:[1,0,1]
	s_nop 0
	v_pk_mul_f32 v[36:37], v[32:33], v[34:35] op_sel:[1,1] op_sel_hi:[0,1] neg_hi:[1,0]
	s_nop 0
	v_pk_fma_f32 v[32:33], v[32:33], v[34:35], v[36:37] op_sel_hi:[1,0,1]
	v_pk_mul_f32 v[36:37], v[182:183], v[34:35] op_sel:[1,1] op_sel_hi:[0,1] neg_lo:[0,1]
	v_pk_fma_f32 v[38:39], v[182:183], v[34:35], v[36:37] op_sel_hi:[1,0,1]
	v_xad_u32 v34, v50, 4, v10
	v_lshl_add_u32 v55, v34, 3, 0
	ds_read2_b64 v[34:37], v55 offset0:128 offset1:144
	v_pk_mul_f32 v[40:41], v[182:183], v[38:39] op_sel:[1,1] op_sel_hi:[0,1] neg_lo:[0,1]
	s_waitcnt lgkmcnt(0)
	v_pk_mul_f32 v[42:43], v[34:35], v[38:39] op_sel:[1,1] op_sel_hi:[0,1] neg_hi:[1,0]
	s_nop 0
	v_pk_fma_f32 v[34:35], v[34:35], v[38:39], v[42:43] op_sel_hi:[1,0,1]
	v_pk_fma_f32 v[42:43], v[182:183], v[38:39], v[40:41] op_sel_hi:[1,0,1]
	s_nop 0
	v_pk_mul_f32 v[38:39], v[36:37], v[42:43] op_sel:[1,1] op_sel_hi:[0,1] neg_hi:[1,0]
	v_pk_fma_f32 v[36:37], v[36:37], v[42:43], v[38:39] op_sel_hi:[1,0,1]
	v_xad_u32 v38, v50, 5, v10
	v_lshl_add_u32 v56, v38, 3, 0
	ds_read2_b64 v[38:41], v56 offset0:160 offset1:176
	v_pk_mul_f32 v[44:45], v[182:183], v[42:43] op_sel:[1,1] op_sel_hi:[0,1] neg_lo:[0,1]
	v_pk_fma_f32 v[42:43], v[182:183], v[42:43], v[44:45] op_sel_hi:[1,0,1]
	s_waitcnt lgkmcnt(0)
	v_pk_mul_f32 v[44:45], v[38:39], v[42:43] op_sel:[1,1] op_sel_hi:[0,1] neg_hi:[1,0]
	s_nop 0
	v_pk_fma_f32 v[38:39], v[38:39], v[42:43], v[44:45] op_sel_hi:[1,0,1]
	v_pk_mul_f32 v[44:45], v[182:183], v[42:43] op_sel:[1,1] op_sel_hi:[0,1] neg_lo:[0,1]
	v_pk_fma_f32 v[42:43], v[182:183], v[42:43], v[44:45] op_sel_hi:[1,0,1]
	s_nop 0
	v_pk_mul_f32 v[44:45], v[40:41], v[42:43] op_sel:[1,1] op_sel_hi:[0,1] neg_hi:[1,0]
	s_nop 0
	v_pk_fma_f32 v[40:41], v[40:41], v[42:43], v[44:45] op_sel_hi:[1,0,1]
	v_pk_mul_f32 v[44:45], v[182:183], v[42:43] op_sel:[1,1] op_sel_hi:[0,1] neg_lo:[0,1]
	v_pk_fma_f32 v[42:43], v[182:183], v[42:43], v[44:45] op_sel_hi:[1,0,1]
	v_xad_u32 v44, v50, 6, v10
	v_lshl_add_u32 v57, v44, 3, 0
	ds_read2_b64 v[44:47], v57 offset0:192 offset1:208
	v_pk_mul_f32 v[48:49], v[182:183], v[42:43] op_sel:[1,1] op_sel_hi:[0,1] neg_lo:[0,1]
	s_waitcnt lgkmcnt(0)
	v_pk_mul_f32 v[52:53], v[44:45], v[42:43] op_sel:[1,1] op_sel_hi:[0,1] neg_hi:[1,0]
	s_nop 0
	v_pk_fma_f32 v[44:45], v[44:45], v[42:43], v[52:53] op_sel_hi:[1,0,1]
	v_pk_fma_f32 v[52:53], v[182:183], v[42:43], v[48:49] op_sel_hi:[1,0,1]
	s_nop 0
	v_pk_mul_f32 v[42:43], v[46:47], v[52:53] op_sel:[1,1] op_sel_hi:[0,1] neg_hi:[1,0]
	v_pk_fma_f32 v[42:43], v[46:47], v[52:53], v[42:43] op_sel_hi:[1,0,1]
	v_xad_u32 v46, v50, 7, v10
	v_lshl_add_u32 v58, v46, 3, 0
	ds_read2_b64 v[46:49], v58 offset0:224 offset1:240
	v_pk_mul_f32 v[60:61], v[182:183], v[52:53] op_sel:[1,1] op_sel_hi:[0,1] neg_lo:[0,1]
	v_pk_fma_f32 v[52:53], v[182:183], v[52:53], v[60:61] op_sel_hi:[1,0,1]
	s_waitcnt lgkmcnt(0)
	v_pk_mul_f32 v[60:61], v[46:47], v[52:53] op_sel:[1,1] op_sel_hi:[0,1] neg_hi:[1,0]
	s_nop 0
	v_pk_fma_f32 v[46:47], v[46:47], v[52:53], v[60:61] op_sel_hi:[1,0,1]
	v_pk_mul_f32 v[60:61], v[182:183], v[52:53] op_sel:[1,1] op_sel_hi:[0,1] neg_lo:[0,1]
	v_pk_fma_f32 v[52:53], v[182:183], v[52:53], v[60:61] op_sel_hi:[1,0,1]
	s_nop 0
	v_pk_mul_f32 v[60:61], v[48:49], v[52:53] op_sel:[1,1] op_sel_hi:[0,1] neg_hi:[1,0]
	s_nop 0
	v_pk_fma_f32 v[48:49], v[48:49], v[52:53], v[60:61] op_sel_hi:[1,0,1]
	v_pk_mul_f32 v[60:61], v[182:183], v[52:53] op_sel:[1,1] op_sel_hi:[0,1] neg_lo:[0,1]
	v_pk_fma_f32 v[64:65], v[182:183], v[52:53], v[60:61] op_sel_hi:[1,0,1]
	v_xad_u32 v52, v50, 8, v10
	v_lshl_add_u32 v52, v52, 3, 0
	v_add_u32_e32 v59, 0x800, v52
	ds_read2_b64 v[60:63], v59 offset1:16
	v_pk_mul_f32 v[66:67], v[182:183], v[64:65] op_sel:[1,1] op_sel_hi:[0,1] neg_lo:[0,1]
	v_pk_fma_f32 v[66:67], v[182:183], v[64:65], v[66:67] op_sel_hi:[1,0,1]
	s_waitcnt lgkmcnt(0)
	v_pk_mul_f32 v[52:53], v[60:61], v[64:65] op_sel:[1,1] op_sel_hi:[0,1] neg_hi:[1,0]
	v_pk_fma_f32 v[52:53], v[60:61], v[64:65], v[52:53] op_sel_hi:[1,0,1]
	v_pk_mul_f32 v[60:61], v[62:63], v[66:67] op_sel:[1,1] op_sel_hi:[0,1] neg_hi:[1,0]
	v_pk_fma_f32 v[70:71], v[62:63], v[66:67], v[60:61] op_sel_hi:[1,0,1]
	v_xad_u32 v60, v50, 9, v10
	v_lshl_add_u32 v60, v60, 3, 0
	v_add_u32_e32 v60, 0x800, v60
	ds_read2_b64 v[62:65], v60 offset0:32 offset1:48
	v_pk_mul_f32 v[68:69], v[182:183], v[66:67] op_sel:[1,1] op_sel_hi:[0,1] neg_lo:[0,1]
	v_pk_fma_f32 v[66:67], v[182:183], v[66:67], v[68:69] op_sel_hi:[1,0,1]
	s_waitcnt lgkmcnt(0)
	v_pk_mul_f32 v[68:69], v[62:63], v[66:67] op_sel:[1,1] op_sel_hi:[0,1] neg_hi:[1,0]
	s_nop 0
	v_pk_fma_f32 v[72:73], v[62:63], v[66:67], v[68:69] op_sel_hi:[1,0,1]
	v_pk_mul_f32 v[62:63], v[182:183], v[66:67] op_sel:[1,1] op_sel_hi:[0,1] neg_lo:[0,1]
	v_pk_fma_f32 v[62:63], v[182:183], v[66:67], v[62:63] op_sel_hi:[1,0,1]
	s_nop 0
	v_pk_mul_f32 v[66:67], v[64:65], v[62:63] op_sel:[1,1] op_sel_hi:[0,1] neg_hi:[1,0]
	s_nop 0
	v_pk_fma_f32 v[74:75], v[64:65], v[62:63], v[66:67] op_sel_hi:[1,0,1]
	v_pk_mul_f32 v[64:65], v[182:183], v[62:63] op_sel:[1,1] op_sel_hi:[0,1] neg_lo:[0,1]
	v_pk_fma_f32 v[66:67], v[182:183], v[62:63], v[64:65] op_sel_hi:[1,0,1]
	v_xad_u32 v61, v50, 10, v10
	v_lshl_add_u32 v61, v61, 3, 0
	v_add_u32_e32 v61, 0x800, v61
	ds_read2_b64 v[62:65], v61 offset0:64 offset1:80
	v_pk_mul_f32 v[68:69], v[182:183], v[66:67] op_sel:[1,1] op_sel_hi:[0,1] neg_lo:[0,1]
	v_pk_fma_f32 v[68:69], v[182:183], v[66:67], v[68:69] op_sel_hi:[1,0,1]
	s_waitcnt lgkmcnt(0)
	v_pk_mul_f32 v[76:77], v[62:63], v[66:67] op_sel:[1,1] op_sel_hi:[0,1] neg_hi:[1,0]
	v_pk_fma_f32 v[76:77], v[62:63], v[66:67], v[76:77] op_sel_hi:[1,0,1]
	v_pk_mul_f32 v[62:63], v[64:65], v[68:69] op_sel:[1,1] op_sel_hi:[0,1] neg_hi:[1,0]
	v_pk_fma_f32 v[78:79], v[64:65], v[68:69], v[62:63] op_sel_hi:[1,0,1]
	v_xad_u32 v62, v50, 11, v10
	v_lshl_add_u32 v62, v62, 3, 0
	v_add_u32_e32 v62, 0x800, v62
	ds_read2_b64 v[64:67], v62 offset0:96 offset1:112
	v_pk_mul_f32 v[80:81], v[182:183], v[68:69] op_sel:[1,1] op_sel_hi:[0,1] neg_lo:[0,1]
	v_pk_fma_f32 v[68:69], v[182:183], v[68:69], v[80:81] op_sel_hi:[1,0,1]
	s_waitcnt lgkmcnt(0)
	v_pk_mul_f32 v[80:81], v[64:65], v[68:69] op_sel:[1,1] op_sel_hi:[0,1] neg_hi:[1,0]
	s_nop 0
	v_pk_fma_f32 v[80:81], v[64:65], v[68:69], v[80:81] op_sel_hi:[1,0,1]
	v_pk_mul_f32 v[64:65], v[182:183], v[68:69] op_sel:[1,1] op_sel_hi:[0,1] neg_lo:[0,1]
	v_pk_fma_f32 v[64:65], v[182:183], v[68:69], v[64:65] op_sel_hi:[1,0,1]
	s_nop 0
	v_pk_mul_f32 v[68:69], v[66:67], v[64:65] op_sel:[1,1] op_sel_hi:[0,1] neg_hi:[1,0]
	s_nop 0
	v_pk_fma_f32 v[82:83], v[66:67], v[64:65], v[68:69] op_sel_hi:[1,0,1]
	v_pk_mul_f32 v[66:67], v[182:183], v[64:65] op_sel:[1,1] op_sel_hi:[0,1] neg_lo:[0,1]
	v_pk_fma_f32 v[68:69], v[182:183], v[64:65], v[66:67] op_sel_hi:[1,0,1]
	v_xad_u32 v63, v50, 12, v10
	v_lshl_add_u32 v63, v63, 3, 0
	v_add_u32_e32 v63, 0x800, v63
	ds_read2_b64 v[64:67], v63 offset0:128 offset1:144
	v_pk_mul_f32 v[84:85], v[182:183], v[68:69] op_sel:[1,1] op_sel_hi:[0,1] neg_lo:[0,1]
	v_pk_fma_f32 v[84:85], v[182:183], v[68:69], v[84:85] op_sel_hi:[1,0,1]
	s_waitcnt lgkmcnt(0)
	v_pk_mul_f32 v[86:87], v[64:65], v[68:69] op_sel:[1,1] op_sel_hi:[0,1] neg_hi:[1,0]
	v_pk_fma_f32 v[86:87], v[64:65], v[68:69], v[86:87] op_sel_hi:[1,0,1]
	v_pk_mul_f32 v[64:65], v[66:67], v[84:85] op_sel:[1,1] op_sel_hi:[0,1] neg_hi:[1,0]
	v_pk_fma_f32 v[88:89], v[66:67], v[84:85], v[64:65] op_sel_hi:[1,0,1]
	v_xad_u32 v64, v50, 13, v10
	v_lshl_add_u32 v64, v64, 3, 0
	v_add_u32_e32 v64, 0x800, v64
	ds_read2_b64 v[66:69], v64 offset0:160 offset1:176
	v_pk_mul_f32 v[90:91], v[182:183], v[84:85] op_sel:[1,1] op_sel_hi:[0,1] neg_lo:[0,1]
	v_pk_fma_f32 v[84:85], v[182:183], v[84:85], v[90:91] op_sel_hi:[1,0,1]
	s_waitcnt lgkmcnt(0)
	v_pk_mul_f32 v[90:91], v[66:67], v[84:85] op_sel:[1,1] op_sel_hi:[0,1] neg_hi:[1,0]
	s_nop 0
	v_pk_fma_f32 v[90:91], v[66:67], v[84:85], v[90:91] op_sel_hi:[1,0,1]
	v_pk_mul_f32 v[66:67], v[182:183], v[84:85] op_sel:[1,1] op_sel_hi:[0,1] neg_lo:[0,1]
	v_pk_fma_f32 v[66:67], v[182:183], v[84:85], v[66:67] op_sel_hi:[1,0,1]
	s_nop 0
	v_pk_mul_f32 v[84:85], v[68:69], v[66:67] op_sel:[1,1] op_sel_hi:[0,1] neg_hi:[1,0]
	s_nop 0
	v_pk_fma_f32 v[84:85], v[68:69], v[66:67], v[84:85] op_sel_hi:[1,0,1]
	v_pk_mul_f32 v[68:69], v[182:183], v[66:67] op_sel:[1,1] op_sel_hi:[0,1] neg_lo:[0,1]
	v_pk_fma_f32 v[92:93], v[182:183], v[66:67], v[68:69] op_sel_hi:[1,0,1]
	v_xad_u32 v65, v50, 14, v10
	v_lshl_add_u32 v65, v65, 3, 0
	v_add_u32_e32 v65, 0x800, v65
	ds_read2_b64 v[66:69], v65 offset0:192 offset1:208
	v_pk_mul_f32 v[94:95], v[182:183], v[92:93] op_sel:[1,1] op_sel_hi:[0,1] neg_lo:[0,1]
	v_xad_u32 v10, v50, 15, v10
	s_waitcnt lgkmcnt(0)
	v_pk_mul_f32 v[96:97], v[66:67], v[92:93] op_sel:[1,1] op_sel_hi:[0,1] neg_hi:[1,0]
	v_lshl_add_u32 v10, v10, 3, 0
	v_pk_fma_f32 v[96:97], v[66:67], v[92:93], v[96:97] op_sel_hi:[1,0,1]
	v_pk_fma_f32 v[92:93], v[182:183], v[92:93], v[94:95] op_sel_hi:[1,0,1]
	s_nop 0
	v_pk_mul_f32 v[66:67], v[68:69], v[92:93] op_sel:[1,1] op_sel_hi:[0,1] neg_hi:[1,0]
	v_add_u32_e32 v101, 0x800, v10
	v_pk_fma_f32 v[94:95], v[68:69], v[92:93], v[66:67] op_sel_hi:[1,0,1]
	ds_read2_b64 v[66:69], v101 offset0:224 offset1:240
	v_pk_mul_f32 v[98:99], v[182:183], v[92:93] op_sel:[1,1] op_sel_hi:[0,1] neg_lo:[0,1]
	v_pk_fma_f32 v[92:93], v[182:183], v[92:93], v[98:99] op_sel_hi:[1,0,1]
	s_waitcnt lgkmcnt(0)
	v_pk_mul_f32 v[98:99], v[66:67], v[92:93] op_sel:[1,1] op_sel_hi:[0,1] neg_hi:[1,0]
	s_nop 0
	v_pk_fma_f32 v[66:67], v[66:67], v[92:93], v[98:99] op_sel_hi:[1,0,1]
	v_pk_mul_f32 v[98:99], v[182:183], v[92:93] op_sel:[1,1] op_sel_hi:[0,1] neg_lo:[0,1]
	v_pk_fma_f32 v[20:21], v[182:183], v[92:93], v[98:99] op_sel_hi:[1,0,1]
	s_nop 0
	v_pk_mul_f32 v[92:93], v[68:69], v[20:21] op_sel:[1,1] op_sel_hi:[0,1] neg_hi:[1,0]
	s_nop 0
	v_pk_fma_f32 v[68:69], v[68:69], v[20:21], v[92:93] op_sel_hi:[1,0,1]
	v_mov_b32_e32 v10, v164
	v_pk_add_f32 v[104:105], v[16:17], v[52:53]
	v_pk_add_f32 v[16:17], v[16:17], v[52:53] neg_lo:[0,1] neg_hi:[0,1]
	v_pk_add_f32 v[52:53], v[18:19], v[70:71]
	v_pk_add_f32 v[18:19], v[18:19], v[70:71] neg_lo:[0,1] neg_hi:[0,1]
	v_mov_b32_e32 v92, v165
	v_mov_b32_e32 v20, v166
	v_mov_b32_e32 v98, v167
	v_mov_b32_e32 v10, v168
	v_mov_b32_e32 v100, v169
	v_mov_b32_e32 v50, v170
	v_mov_b32_e32 v102, v171
	v_mov_b32_e32 v21, v172
	v_pk_mul_f32 v[70:71], v[102:103], v[18:19] op_sel:[0,1] op_sel_hi:[0,0] neg_lo:[0,1]
	v_pk_fma_f32 v[18:19], v[92:93], v[18:19], v[70:71] op_sel_hi:[0,1,1]
	v_pk_add_f32 v[70:71], v[22:23], v[72:73]
	v_pk_add_f32 v[22:23], v[22:23], v[72:73] neg_lo:[0,1] neg_hi:[0,1]
	s_nop 0
	v_pk_mul_f32 v[72:73], v[50:51], v[22:23] op_sel:[0,1] op_sel_hi:[0,0] neg_lo:[0,1]
	v_pk_fma_f32 v[22:23], v[20:21], v[22:23], v[72:73] op_sel_hi:[0,1,1]
	v_pk_add_f32 v[72:73], v[24:25], v[74:75]
	v_pk_add_f32 v[24:25], v[24:25], v[74:75] neg_lo:[0,1] neg_hi:[0,1]
	s_nop 0
	v_pk_mul_f32 v[74:75], v[100:101], v[24:25] op_sel:[0,1] op_sel_hi:[0,0] neg_lo:[0,1]
	v_pk_fma_f32 v[24:25], v[98:99], v[24:25], v[74:75] op_sel_hi:[0,1,1]
	v_pk_add_f32 v[74:75], v[28:29], v[76:77]
	v_pk_add_f32 v[28:29], v[28:29], v[76:77] neg_lo:[0,1] neg_hi:[0,1]
	s_nop 0
	v_pk_mul_f32 v[76:77], v[10:11], v[28:29] op_sel:[0,1] op_sel_hi:[0,0] neg_lo:[0,1]
	v_pk_fma_f32 v[28:29], v[10:11], v[28:29], v[76:77] op_sel_hi:[0,1,1]
	v_pk_add_f32 v[76:77], v[26:27], v[78:79]
	v_pk_add_f32 v[26:27], v[26:27], v[78:79] neg_lo:[0,1] neg_hi:[0,1]
	s_nop 0
	v_pk_mul_f32 v[78:79], v[98:99], v[26:27] op_sel:[0,1] op_sel_hi:[0,0] neg_lo:[0,1]
	v_pk_fma_f32 v[26:27], v[100:101], v[26:27], v[78:79] op_sel_hi:[0,1,1]
	v_pk_add_f32 v[78:79], v[30:31], v[80:81]
	v_pk_add_f32 v[30:31], v[30:31], v[80:81] neg_lo:[0,1] neg_hi:[0,1]
	s_nop 0
	v_pk_mul_f32 v[80:81], v[20:21], v[30:31] op_sel:[0,1] op_sel_hi:[0,0] neg_lo:[0,1]
	v_pk_fma_f32 v[30:31], v[50:51], v[30:31], v[80:81] op_sel_hi:[0,1,1]
	v_pk_add_f32 v[80:81], v[32:33], v[82:83]
	v_pk_add_f32 v[32:33], v[32:33], v[82:83] neg_lo:[0,1] neg_hi:[0,1]
	s_nop 0
	v_pk_mul_f32 v[82:83], v[92:93], v[32:33] op_sel:[0,1] op_sel_hi:[0,0] neg_lo:[0,1]
	v_pk_fma_f32 v[32:33], v[102:103], v[32:33], v[82:83] op_sel_hi:[0,1,1]
	v_pk_add_f32 v[82:83], v[34:35], v[86:87]
	v_pk_add_f32 v[34:35], v[34:35], v[86:87] neg_lo:[0,1] neg_hi:[0,1]
	s_nop 0
	v_xor_b32_e32 v86, 0x80000000, v35
	v_mov_b32_e32 v87, v34
	v_pk_add_f32 v[34:35], v[36:37], v[88:89]
	v_pk_add_f32 v[36:37], v[36:37], v[88:89] neg_lo:[0,1] neg_hi:[0,1]
	s_nop 0
	v_pk_mul_f32 v[88:89], v[92:93], v[36:37] op_sel:[0,1] op_sel_hi:[0,0] neg_lo:[0,1]
	v_pk_fma_f32 v[36:37], v[102:103], v[36:37], v[88:89] op_sel_hi:[0,1,1] neg_lo:[1,0,0] neg_hi:[1,0,0]
	v_pk_add_f32 v[88:89], v[38:39], v[90:91]
	v_pk_add_f32 v[38:39], v[38:39], v[90:91] neg_lo:[0,1] neg_hi:[0,1]
	s_nop 0
	v_pk_mul_f32 v[90:91], v[20:21], v[38:39] op_sel:[0,1] op_sel_hi:[0,0] neg_lo:[0,1]
	v_pk_fma_f32 v[38:39], v[50:51], v[38:39], v[90:91] op_sel_hi:[0,1,1] neg_lo:[1,0,0] neg_hi:[1,0,0]
	v_pk_add_f32 v[90:91], v[40:41], v[84:85]
	v_pk_add_f32 v[40:41], v[40:41], v[84:85] neg_lo:[0,1] neg_hi:[0,1]
	s_nop 0
	v_pk_mul_f32 v[84:85], v[98:99], v[40:41] op_sel:[0,1] op_sel_hi:[0,0] neg_lo:[0,1]
	v_pk_fma_f32 v[40:41], v[100:101], v[40:41], v[84:85] op_sel_hi:[0,1,1] neg_lo:[1,0,0] neg_hi:[1,0,0]
	v_pk_add_f32 v[84:85], v[44:45], v[96:97]
	v_pk_add_f32 v[44:45], v[44:45], v[96:97] neg_lo:[0,1] neg_hi:[0,1]
	s_nop 0
	v_pk_mul_f32 v[96:97], v[10:11], v[44:45] op_sel:[0,1] op_sel_hi:[0,0] neg_lo:[0,1]
	v_pk_fma_f32 v[44:45], v[10:11], v[44:45], v[96:97] op_sel_hi:[0,1,1] neg_lo:[1,0,0] neg_hi:[1,0,0]
	v_pk_add_f32 v[96:97], v[42:43], v[94:95]
	v_pk_add_f32 v[42:43], v[42:43], v[94:95] neg_lo:[0,1] neg_hi:[0,1]
	s_nop 0
	v_pk_mul_f32 v[94:95], v[100:101], v[42:43] op_sel:[0,1] op_sel_hi:[0,0] neg_lo:[0,1]
	v_pk_fma_f32 v[42:43], v[98:99], v[42:43], v[94:95] op_sel_hi:[0,1,1] neg_lo:[1,0,0] neg_hi:[1,0,0]
	v_pk_add_f32 v[94:95], v[46:47], v[66:67]
	v_pk_add_f32 v[46:47], v[46:47], v[66:67] neg_lo:[0,1] neg_hi:[0,1]
	s_nop 0
	v_pk_mul_f32 v[66:67], v[50:51], v[46:47] op_sel:[0,1] op_sel_hi:[0,0] neg_lo:[0,1]
	v_pk_fma_f32 v[46:47], v[20:21], v[46:47], v[66:67] op_sel_hi:[0,1,1] neg_lo:[1,0,0] neg_hi:[1,0,0]
	v_pk_add_f32 v[66:67], v[48:49], v[68:69]
	v_pk_add_f32 v[48:49], v[48:49], v[68:69] neg_lo:[0,1] neg_hi:[0,1]
	s_nop 0
	v_pk_mul_f32 v[68:69], v[102:103], v[48:49] op_sel:[0,1] op_sel_hi:[0,0] neg_lo:[0,1]
	v_pk_fma_f32 v[48:49], v[92:93], v[48:49], v[68:69] op_sel_hi:[0,1,1] neg_lo:[1,0,0] neg_hi:[1,0,0]
	v_pk_add_f32 v[92:93], v[52:53], v[34:35]
	v_pk_add_f32 v[34:35], v[52:53], v[34:35] neg_lo:[0,1] neg_hi:[0,1]
	v_pk_add_f32 v[68:69], v[104:105], v[82:83]
	v_pk_mul_f32 v[52:53], v[50:51], v[34:35] op_sel:[0,1] op_sel_hi:[0,0] neg_lo:[0,1]
	v_pk_fma_f32 v[34:35], v[20:21], v[34:35], v[52:53] op_sel_hi:[0,1,1]
	v_pk_add_f32 v[52:53], v[70:71], v[88:89]
	v_pk_add_f32 v[70:71], v[70:71], v[88:89] neg_lo:[0,1] neg_hi:[0,1]
	v_pk_add_f32 v[82:83], v[104:105], v[82:83] neg_lo:[0,1] neg_hi:[0,1]
	v_pk_mul_f32 v[88:89], v[10:11], v[70:71] op_sel:[0,1] op_sel_hi:[0,0] neg_lo:[0,1]
	v_pk_fma_f32 v[70:71], v[10:11], v[70:71], v[88:89] op_sel_hi:[0,1,1]
	v_pk_add_f32 v[88:89], v[72:73], v[90:91]
	v_pk_add_f32 v[72:73], v[72:73], v[90:91] neg_lo:[0,1] neg_hi:[0,1]
	s_nop 0
	v_pk_mul_f32 v[90:91], v[20:21], v[72:73] op_sel:[0,1] op_sel_hi:[0,0] neg_lo:[0,1]
	v_pk_fma_f32 v[72:73], v[50:51], v[72:73], v[90:91] op_sel_hi:[0,1,1]
	v_pk_add_f32 v[90:91], v[74:75], v[84:85]
	v_pk_add_f32 v[74:75], v[74:75], v[84:85] neg_lo:[0,1] neg_hi:[0,1]
	s_nop 0
	v_xor_b32_e32 v84, 0x80000000, v75
	v_mov_b32_e32 v85, v74
	v_pk_add_f32 v[74:75], v[76:77], v[96:97]
	v_pk_add_f32 v[76:77], v[76:77], v[96:97] neg_lo:[0,1] neg_hi:[0,1]
	s_nop 0
	v_pk_mul_f32 v[96:97], v[20:21], v[76:77] op_sel:[0,1] op_sel_hi:[0,0] neg_lo:[0,1]
	v_pk_fma_f32 v[76:77], v[50:51], v[76:77], v[96:97] op_sel_hi:[0,1,1] neg_lo:[1,0,0] neg_hi:[1,0,0]
	v_pk_add_f32 v[96:97], v[78:79], v[94:95]
	v_pk_add_f32 v[78:79], v[78:79], v[94:95] neg_lo:[0,1] neg_hi:[0,1]
	s_nop 0
	v_pk_mul_f32 v[94:95], v[10:11], v[78:79] op_sel:[0,1] op_sel_hi:[0,0] neg_lo:[0,1]
	v_pk_fma_f32 v[78:79], v[10:11], v[78:79], v[94:95] op_sel_hi:[0,1,1] neg_lo:[1,0,0] neg_hi:[1,0,0]
	v_pk_add_f32 v[94:95], v[80:81], v[66:67]
	v_pk_add_f32 v[66:67], v[80:81], v[66:67] neg_lo:[0,1] neg_hi:[0,1]
	s_nop 0
	v_pk_mul_f32 v[80:81], v[50:51], v[66:67] op_sel:[0,1] op_sel_hi:[0,0] neg_lo:[0,1]
	v_pk_fma_f32 v[66:67], v[20:21], v[66:67], v[80:81] op_sel_hi:[0,1,1] neg_lo:[1,0,0] neg_hi:[1,0,0]
	v_pk_add_f32 v[80:81], v[68:69], v[90:91]
	v_pk_add_f32 v[68:69], v[68:69], v[90:91] neg_lo:[0,1] neg_hi:[0,1]
	v_pk_add_f32 v[90:91], v[92:93], v[74:75]
	v_pk_add_f32 v[74:75], v[92:93], v[74:75] neg_lo:[0,1] neg_hi:[0,1]
	s_nop 0
	v_pk_mul_f32 v[92:93], v[10:11], v[74:75] op_sel:[0,1] op_sel_hi:[0,0] neg_lo:[0,1]
	v_pk_fma_f32 v[74:75], v[10:11], v[74:75], v[92:93] op_sel_hi:[0,1,1]
	v_pk_add_f32 v[92:93], v[52:53], v[96:97]
	v_pk_add_f32 v[52:53], v[52:53], v[96:97] neg_lo:[0,1] neg_hi:[0,1]
	s_nop 0
	v_xor_b32_e32 v96, 0x80000000, v53
	v_mov_b32_e32 v97, v52
	v_pk_add_f32 v[52:53], v[88:89], v[94:95]
	v_pk_add_f32 v[88:89], v[88:89], v[94:95] neg_lo:[0,1] neg_hi:[0,1]
	s_nop 0
	v_pk_mul_f32 v[94:95], v[10:11], v[88:89] op_sel:[0,1] op_sel_hi:[0,0] neg_lo:[0,1]
	v_pk_fma_f32 v[88:89], v[10:11], v[88:89], v[94:95] op_sel_hi:[0,1,1] neg_lo:[1,0,0] neg_hi:[1,0,0]
	v_pk_add_f32 v[94:95], v[80:81], v[92:93]
	v_pk_add_f32 v[80:81], v[80:81], v[92:93] neg_lo:[0,1] neg_hi:[0,1]
	v_pk_add_f32 v[92:93], v[90:91], v[52:53]
	v_pk_add_f32 v[52:53], v[90:91], v[52:53] neg_lo:[0,1] neg_hi:[0,1]
	s_nop 0
	v_xor_b32_e32 v90, 0x80000000, v53
	v_mov_b32_e32 v91, v52
	v_pk_add_f32 v[52:53], v[94:95], v[92:93]
	v_pk_add_f32 v[92:93], v[94:95], v[92:93] neg_lo:[0,1] neg_hi:[0,1]
	v_pk_add_f32 v[94:95], v[80:81], v[90:91]
	v_pk_add_f32 v[80:81], v[80:81], v[90:91] neg_lo:[0,1] neg_hi:[0,1]
	v_pk_add_f32 v[90:91], v[68:69], v[96:97]
	v_pk_add_f32 v[68:69], v[68:69], v[96:97] neg_lo:[0,1] neg_hi:[0,1]
	v_pk_add_f32 v[96:97], v[74:75], v[88:89]
	v_pk_add_f32 v[74:75], v[74:75], v[88:89] neg_lo:[0,1] neg_hi:[0,1]
	s_nop 0
	v_xor_b32_e32 v88, 0x80000000, v75
	v_mov_b32_e32 v89, v74
	v_pk_add_f32 v[74:75], v[90:91], v[96:97]
	v_pk_add_f32 v[90:91], v[90:91], v[96:97] neg_lo:[0,1] neg_hi:[0,1]
	v_pk_add_f32 v[96:97], v[68:69], v[88:89]
	v_pk_add_f32 v[68:69], v[68:69], v[88:89] neg_lo:[0,1] neg_hi:[0,1]
	v_pk_add_f32 v[88:89], v[82:83], v[84:85]
	v_pk_add_f32 v[82:83], v[82:83], v[84:85] neg_lo:[0,1] neg_hi:[0,1]
	v_pk_add_f32 v[84:85], v[34:35], v[76:77]
	v_pk_add_f32 v[34:35], v[34:35], v[76:77] neg_lo:[0,1] neg_hi:[0,1]
	s_nop 0
	v_pk_mul_f32 v[76:77], v[10:11], v[34:35] op_sel:[0,1] op_sel_hi:[0,0] neg_lo:[0,1]
	v_pk_fma_f32 v[34:35], v[10:11], v[34:35], v[76:77] op_sel_hi:[0,1,1]
	v_pk_add_f32 v[76:77], v[70:71], v[78:79]
	v_pk_add_f32 v[70:71], v[70:71], v[78:79] neg_lo:[0,1] neg_hi:[0,1]
	s_nop 0
	v_xor_b32_e32 v78, 0x80000000, v71
	v_mov_b32_e32 v79, v70
	v_pk_add_f32 v[70:71], v[72:73], v[66:67]
	v_pk_add_f32 v[66:67], v[72:73], v[66:67] neg_lo:[0,1] neg_hi:[0,1]
	s_nop 0
	v_pk_mul_f32 v[72:73], v[10:11], v[66:67] op_sel:[0,1] op_sel_hi:[0,0] neg_lo:[0,1]
	v_pk_fma_f32 v[66:67], v[10:11], v[66:67], v[72:73] op_sel_hi:[0,1,1] neg_lo:[1,0,0] neg_hi:[1,0,0]
	v_pk_add_f32 v[72:73], v[88:89], v[76:77]
	v_pk_add_f32 v[76:77], v[88:89], v[76:77] neg_lo:[0,1] neg_hi:[0,1]
	v_pk_add_f32 v[88:89], v[84:85], v[70:71]
	v_pk_add_f32 v[70:71], v[84:85], v[70:71] neg_lo:[0,1] neg_hi:[0,1]
	s_nop 0
	v_xor_b32_e32 v84, 0x80000000, v71
	v_mov_b32_e32 v85, v70
	v_pk_add_f32 v[70:71], v[72:73], v[88:89]
	v_pk_add_f32 v[72:73], v[72:73], v[88:89] neg_lo:[0,1] neg_hi:[0,1]
	v_pk_add_f32 v[88:89], v[76:77], v[84:85]
	v_pk_add_f32 v[76:77], v[76:77], v[84:85] neg_lo:[0,1] neg_hi:[0,1]
	v_pk_add_f32 v[84:85], v[82:83], v[78:79]
	v_pk_add_f32 v[78:79], v[82:83], v[78:79] neg_lo:[0,1] neg_hi:[0,1]
	v_pk_add_f32 v[82:83], v[34:35], v[66:67]
	v_pk_add_f32 v[34:35], v[34:35], v[66:67] neg_lo:[0,1] neg_hi:[0,1]
	s_nop 0
	v_xor_b32_e32 v66, 0x80000000, v35
	v_mov_b32_e32 v67, v34
	v_pk_add_f32 v[34:35], v[84:85], v[82:83]
	v_pk_add_f32 v[82:83], v[84:85], v[82:83] neg_lo:[0,1] neg_hi:[0,1]
	v_pk_add_f32 v[84:85], v[78:79], v[66:67]
	v_pk_add_f32 v[66:67], v[78:79], v[66:67] neg_lo:[0,1] neg_hi:[0,1]
	v_pk_add_f32 v[78:79], v[16:17], v[86:87]
	v_pk_add_f32 v[16:17], v[16:17], v[86:87] neg_lo:[0,1] neg_hi:[0,1]
	v_pk_add_f32 v[86:87], v[18:19], v[36:37]
	v_pk_add_f32 v[18:19], v[18:19], v[36:37] neg_lo:[0,1] neg_hi:[0,1]
	s_nop 0
	v_pk_mul_f32 v[36:37], v[50:51], v[18:19] op_sel:[0,1] op_sel_hi:[0,0] neg_lo:[0,1]
	v_pk_fma_f32 v[18:19], v[20:21], v[18:19], v[36:37] op_sel_hi:[0,1,1]
	v_pk_add_f32 v[36:37], v[22:23], v[38:39]
	v_pk_add_f32 v[22:23], v[22:23], v[38:39] neg_lo:[0,1] neg_hi:[0,1]
	s_nop 0
	v_pk_mul_f32 v[38:39], v[10:11], v[22:23] op_sel:[0,1] op_sel_hi:[0,0] neg_lo:[0,1]
	v_pk_fma_f32 v[22:23], v[10:11], v[22:23], v[38:39] op_sel_hi:[0,1,1]
	v_pk_add_f32 v[38:39], v[24:25], v[40:41]
	v_pk_add_f32 v[24:25], v[24:25], v[40:41] neg_lo:[0,1] neg_hi:[0,1]
	s_nop 0
	v_pk_mul_f32 v[40:41], v[20:21], v[24:25] op_sel:[0,1] op_sel_hi:[0,0] neg_lo:[0,1]
	v_pk_fma_f32 v[24:25], v[50:51], v[24:25], v[40:41] op_sel_hi:[0,1,1]
	v_pk_add_f32 v[40:41], v[28:29], v[44:45]
	v_pk_add_f32 v[28:29], v[28:29], v[44:45] neg_lo:[0,1] neg_hi:[0,1]
	s_nop 0
	v_xor_b32_e32 v44, 0x80000000, v29
	v_mov_b32_e32 v45, v28
	v_pk_add_f32 v[28:29], v[26:27], v[42:43]
	v_pk_add_f32 v[26:27], v[26:27], v[42:43] neg_lo:[0,1] neg_hi:[0,1]
	s_nop 0
	v_pk_mul_f32 v[42:43], v[20:21], v[26:27] op_sel:[0,1] op_sel_hi:[0,0] neg_lo:[0,1]
	v_pk_fma_f32 v[26:27], v[50:51], v[26:27], v[42:43] op_sel_hi:[0,1,1] neg_lo:[1,0,0] neg_hi:[1,0,0]
	v_pk_add_f32 v[42:43], v[30:31], v[46:47]
	v_pk_add_f32 v[30:31], v[30:31], v[46:47] neg_lo:[0,1] neg_hi:[0,1]
	s_nop 0
	v_pk_mul_f32 v[46:47], v[10:11], v[30:31] op_sel:[0,1] op_sel_hi:[0,0] neg_lo:[0,1]
	v_pk_fma_f32 v[30:31], v[10:11], v[30:31], v[46:47] op_sel_hi:[0,1,1] neg_lo:[1,0,0] neg_hi:[1,0,0]
	v_pk_add_f32 v[46:47], v[32:33], v[48:49]
	v_pk_add_f32 v[32:33], v[32:33], v[48:49] neg_lo:[0,1] neg_hi:[0,1]
	s_nop 0
	v_pk_mul_f32 v[48:49], v[50:51], v[32:33] op_sel:[0,1] op_sel_hi:[0,0] neg_lo:[0,1]
	v_pk_fma_f32 v[20:21], v[20:21], v[32:33], v[48:49] op_sel_hi:[0,1,1] neg_lo:[1,0,0] neg_hi:[1,0,0]
	v_pk_add_f32 v[48:49], v[86:87], v[28:29]
	v_pk_add_f32 v[28:29], v[86:87], v[28:29] neg_lo:[0,1] neg_hi:[0,1]
	v_pk_add_f32 v[32:33], v[78:79], v[40:41]
	v_pk_add_f32 v[40:41], v[78:79], v[40:41] neg_lo:[0,1] neg_hi:[0,1]
	v_pk_mul_f32 v[78:79], v[10:11], v[28:29] op_sel:[0,1] op_sel_hi:[0,0] neg_lo:[0,1]
	v_pk_fma_f32 v[28:29], v[10:11], v[28:29], v[78:79] op_sel_hi:[0,1,1]
	v_pk_add_f32 v[78:79], v[36:37], v[42:43]
	v_pk_add_f32 v[36:37], v[36:37], v[42:43] neg_lo:[0,1] neg_hi:[0,1]
	s_nop 0
	v_xor_b32_e32 v42, 0x80000000, v37
	v_mov_b32_e32 v43, v36
	v_pk_add_f32 v[36:37], v[38:39], v[46:47]
	v_pk_add_f32 v[38:39], v[38:39], v[46:47] neg_lo:[0,1] neg_hi:[0,1]
	s_nop 0
	v_pk_mul_f32 v[46:47], v[10:11], v[38:39] op_sel:[0,1] op_sel_hi:[0,0] neg_lo:[0,1]
	v_pk_fma_f32 v[38:39], v[10:11], v[38:39], v[46:47] op_sel_hi:[0,1,1] neg_lo:[1,0,0] neg_hi:[1,0,0]
	v_pk_add_f32 v[46:47], v[32:33], v[78:79]
	v_pk_add_f32 v[32:33], v[32:33], v[78:79] neg_lo:[0,1] neg_hi:[0,1]
	v_pk_add_f32 v[78:79], v[48:49], v[36:37]
	v_pk_add_f32 v[36:37], v[48:49], v[36:37] neg_lo:[0,1] neg_hi:[0,1]
	s_nop 0
	v_pk_add_f32 v[86:87], v[32:33], v[36:37] op_sel:[0,1] op_sel_hi:[1,0] neg_lo:[0,1]
	v_pk_add_f32 v[32:33], v[32:33], v[36:37] op_sel:[0,1] op_sel_hi:[1,0] neg_hi:[0,1]
	v_pk_add_f32 v[48:49], v[40:41], v[42:43]
	v_pk_add_f32 v[40:41], v[40:41], v[42:43] neg_lo:[0,1] neg_hi:[0,1]
	v_pk_add_f32 v[42:43], v[28:29], v[38:39]
	v_pk_add_f32 v[28:29], v[28:29], v[38:39] neg_lo:[0,1] neg_hi:[0,1]
	v_pk_add_f32 v[36:37], v[46:47], v[78:79] neg_lo:[0,1] neg_hi:[0,1]
	v_xor_b32_e32 v38, 0x80000000, v29
	v_mov_b32_e32 v39, v28
	v_pk_add_f32 v[28:29], v[48:49], v[42:43]
	v_pk_add_f32 v[42:43], v[48:49], v[42:43] neg_lo:[0,1] neg_hi:[0,1]
	v_pk_add_f32 v[48:49], v[40:41], v[38:39]
	v_pk_add_f32 v[38:39], v[40:41], v[38:39] neg_lo:[0,1] neg_hi:[0,1]
	v_pk_add_f32 v[40:41], v[16:17], v[44:45]
	v_pk_add_f32 v[16:17], v[16:17], v[44:45] neg_lo:[0,1] neg_hi:[0,1]
	v_pk_add_f32 v[44:45], v[18:19], v[26:27]
	v_pk_add_f32 v[18:19], v[18:19], v[26:27] neg_lo:[0,1] neg_hi:[0,1]
	s_nop 0
	v_pk_mul_f32 v[26:27], v[10:11], v[18:19] op_sel:[0,1] op_sel_hi:[0,0] neg_lo:[0,1]
	v_pk_fma_f32 v[18:19], v[10:11], v[18:19], v[26:27] op_sel_hi:[0,1,1]
	v_pk_add_f32 v[26:27], v[22:23], v[30:31]
	v_pk_add_f32 v[22:23], v[22:23], v[30:31] neg_lo:[0,1] neg_hi:[0,1]
	s_nop 0
	v_xor_b32_e32 v30, 0x80000000, v23
	v_mov_b32_e32 v31, v22
	v_pk_add_f32 v[22:23], v[24:25], v[20:21]
	v_pk_add_f32 v[20:21], v[24:25], v[20:21] neg_lo:[0,1] neg_hi:[0,1]
	s_nop 0
	v_pk_mul_f32 v[24:25], v[10:11], v[20:21] op_sel:[0,1] op_sel_hi:[0,0] neg_lo:[0,1]
	v_pk_fma_f32 v[20:21], v[10:11], v[20:21], v[24:25] op_sel_hi:[0,1,1] neg_lo:[1,0,0] neg_hi:[1,0,0]
	v_pk_add_f32 v[24:25], v[40:41], v[26:27]
	v_pk_add_f32 v[26:27], v[40:41], v[26:27] neg_lo:[0,1] neg_hi:[0,1]
	v_pk_add_f32 v[40:41], v[44:45], v[22:23]
	v_pk_add_f32 v[22:23], v[44:45], v[22:23] neg_lo:[0,1] neg_hi:[0,1]
	s_nop 0
	v_xor_b32_e32 v44, 0x80000000, v23
	v_mov_b32_e32 v45, v22
	v_pk_add_f32 v[22:23], v[24:25], v[40:41]
	v_pk_add_f32 v[24:25], v[24:25], v[40:41] neg_lo:[0,1] neg_hi:[0,1]
	v_pk_add_f32 v[40:41], v[26:27], v[44:45]
	v_pk_add_f32 v[26:27], v[26:27], v[44:45] neg_lo:[0,1] neg_hi:[0,1]
	v_pk_add_f32 v[44:45], v[16:17], v[30:31]
	v_pk_add_f32 v[16:17], v[16:17], v[30:31] neg_lo:[0,1] neg_hi:[0,1]
	v_pk_add_f32 v[30:31], v[18:19], v[20:21]
	v_pk_add_f32 v[18:19], v[18:19], v[20:21] neg_lo:[0,1] neg_hi:[0,1]
	s_nop 0
	v_xor_b32_e32 v20, 0x80000000, v19
	v_mov_b32_e32 v21, v18
	v_pk_add_f32 v[18:19], v[44:45], v[30:31]
	v_pk_add_f32 v[30:31], v[44:45], v[30:31] neg_lo:[0,1] neg_hi:[0,1]
	v_pk_add_f32 v[44:45], v[16:17], v[20:21]
	v_pk_add_f32 v[16:17], v[16:17], v[20:21] neg_lo:[0,1] neg_hi:[0,1]
	v_pk_add_f32 v[20:21], v[46:47], v[78:79]
	ds_write2_b64 v13, v[52:53], v[20:21] offset1:16
	ds_write2_b64 v15, v[70:71], v[22:23] offset0:32 offset1:48
	ds_write2_b64 v51, v[74:75], v[28:29] offset0:64 offset1:80
	ds_write2_b64 v54, v[34:35], v[18:19] offset0:96 offset1:112
	ds_write2_b64 v55, v[94:95], v[86:87] offset0:128 offset1:144
	ds_write2_b64 v56, v[88:89], v[40:41] offset0:160 offset1:176
	ds_write2_b64 v57, v[96:97], v[48:49] offset0:192 offset1:208
	ds_write2_b64 v58, v[84:85], v[44:45] offset0:224 offset1:240
	ds_write2_b64 v59, v[92:93], v[36:37] offset1:16
	ds_write2_b64 v60, v[72:73], v[24:25] offset0:32 offset1:48
	ds_write2_b64 v61, v[90:91], v[42:43] offset0:64 offset1:80
	ds_write2_b64 v62, v[82:83], v[30:31] offset0:96 offset1:112
	ds_write2_b64 v63, v[80:81], v[32:33] offset0:128 offset1:144
	ds_write2_b64 v64, v[76:77], v[26:27] offset0:160 offset1:176
	ds_write2_b64 v65, v[68:69], v[38:39] offset0:192 offset1:208
	ds_write2_b64 v101, v[66:67], v[16:17] offset0:224 offset1:240
	v_mov_b32_e32 v10, v174
	s_waitcnt lgkmcnt(0)
	s_barrier
	v_mov_b32_e32 v58, v180
	v_mov_b32_e32 v59, v181
	v_lshl_add_u32 v10, v10, 3, 0
	ds_read_b64 v[34:35], v10
	ds_read_b64 v[36:37], v10 offset:4224
	ds_read_b64 v[38:39], v10 offset:8448
	ds_read_b64 v[40:41], v10 offset:12672
	ds_read_b64 v[42:43], v10 offset:16896
	ds_read_b64 v[44:45], v10 offset:21120
	ds_read_b64 v[50:51], v10 offset:25344
	ds_read_b64 v[52:53], v10 offset:29568
	ds_read_b64 v[54:55], v10 offset:33792
	ds_read_b64 v[56:57], v10 offset:38016
	ds_read_b64 v[64:65], v10 offset:42240
	ds_read_b64 v[74:75], v10 offset:46464
	ds_read_b64 v[76:77], v10 offset:50688
	ds_read_b64 v[78:79], v10 offset:54912
	ds_read_b64 v[80:81], v10 offset:59136
	ds_read_b64 v[82:83], v10 offset:63360
	v_add_u32_e32 v13, 0x10800, v10
	v_add_u32_e32 v15, 0x11880, v10
	v_add_u32_e32 v16, 0x12900, v10
	v_add_u32_e32 v17, 0x13980, v10
	ds_read_b64 v[84:85], v13
	ds_read_b64 v[86:87], v15
	ds_read_b64 v[88:89], v16
	ds_read_b64 v[92:93], v17
	v_add_u32_e32 v13, 0x14a00, v10
	v_add_u32_e32 v15, 0x15a80, v10
	v_add_u32_e32 v16, 0x16b00, v10
	v_add_u32_e32 v17, 0x17b80, v10
	ds_read_b64 v[96:97], v13
	ds_read_b64 v[98:99], v15
	ds_read_b64 v[94:95], v16
	ds_read_b64 v[90:91], v17
	v_add_u32_e32 v13, 0x18c00, v10
	v_add_u32_e32 v15, 0x19c80, v10
	v_add_u32_e32 v16, 0x1ad00, v10
	v_add_u32_e32 v17, 0x1bd80, v10
	ds_read_b64 v[72:73], v13
	ds_read_b64 v[70:71], v15
	ds_read_b64 v[68:69], v16
	ds_read_b64 v[66:67], v17
	v_add_u32_e32 v13, 0x1ce00, v10
	v_add_u32_e32 v15, 0x1de80, v10
	v_add_u32_e32 v16, 0x1ef00, v10
	v_add_u32_e32 v10, 0x1ff80, v10
	ds_read_b64 v[62:63], v13
	ds_read_b64 v[60:61], v15
	ds_read_b64 v[100:101], v16
	ds_read_b64 v[102:103], v10
	s_mov_b32 s45, s43
	v_mov_b32_e32 v10, v164
	s_lshl_b64 s[0:1], s[44:45], 2
	v_readlane_b32 s2, v251, 40
	s_add_u32 s0, s2, s0
	v_readlane_b32 s2, v251, 46
	v_mov_b32_e32 v24, v165
	v_mov_b32_e32 v32, v166
	v_mov_b32_e32 v28, v167
	v_mov_b32_e32 v46, v168
	v_mov_b32_e32 v48, v169
	v_mov_b32_e32 v30, v170
	v_mov_b32_e32 v26, v171
	v_mov_b32_e32 v10, v172
	v_mov_b32_e32 v16, v184
	v_mov_b32_e32 v19, v185
	s_addc_u32 s1, s2, s1
	s_waitcnt lgkmcnt(0)
	s_barrier
	global_load_dword v13, v11, s[0:1]
	s_and_b64 s[0:1], s[96:97], exec
	s_movk_i32 s0, 0x800
	s_cselect_b32 s2, 0x400, s0
	v_readlane_b32 s20, v251, 36
	s_add_i32 s4, s2, s20
	s_mul_i32 s0, s4, 0x8200
	v_readlane_b32 s3, v250, 23
	s_mul_hi_i32 s1, s4, 0x8200
	s_add_u32 s0, s3, s0
	v_readlane_b32 s3, v251, 20
	s_addc_u32 s1, s3, s1
	s_lshl_b32 s2, s2, 2
	v_mov_b32_e32 v10, s2
	v_readlane_b32 s2, v251, 50
	v_readlane_b32 s3, v251, 51
	v_readlane_b32 s5, v251, 52
	v_readlane_b32 s6, v251, 18
	v_ashrrev_i32_e32 v15, 31, v14
	v_lshl_add_u64 v[22:23], v[14:15], 2, s[72:73]
	v_cmp_lt_i32_e32 vcc, 0, v14
	global_load_dword v189, v10, s[2:3]
	s_add_i32 s2, s4, 0xc00
	s_ashr_i32 s3, s2, 31
	s_lshl_b64 s[2:3], s[2:3], 2
	s_add_u32 s2, s5, s2
	s_addc_u32 s3, s6, s3
	global_load_dword v191, v11, s[2:3]
	s_add_i32 s2, s4, 0x1800
	s_ashr_i32 s3, s2, 31
	s_lshl_b64 s[2:3], s[2:3], 2
	s_add_u32 s2, s5, s2
	s_addc_u32 s3, s6, s3
	global_load_dword v192, v11, s[2:3]
	v_readlane_b32 s2, v251, 42
	v_readlane_b32 s3, v251, 43
	v_mov_b32_e32 v17, 0
	v_lshl_add_u64 v[20:21], v[14:15], 1, s[0:1]
	v_mov_b32_e32 v18, 0
	v_readlane_b32 s21, v251, 37
	s_nop 0
	global_load_dword v193, v10, s[2:3]
	s_nop 0
	v_lshlrev_b32_e32 v234, 1, v14
	v_lshlrev_b32_e32 v235, 2, v14
	v_add_u32_e32 v235, 0x1000, v235
	global_load_dword v190, v235, s[72:73] offset:-4096
	global_load_ushort v195, v234, s[0:1] offset:-2
	global_load_ushort v196, v234, s[0:1]
	global_load_ushort v197, v234, s[0:1] offset:2
	global_load_dword v198, v235, s[66:67] offset:-4096
	global_load_dword v199, v235, s[72:73] offset:-2048
	global_load_ushort v200, v234, s[0:1] offset:1022
	global_load_ushort v201, v234, s[0:1] offset:1024
	global_load_ushort v202, v234, s[0:1] offset:1026
	global_load_dword v203, v235, s[66:67] offset:-2048
	global_load_dword v204, v235, s[72:73]
	global_load_ushort v205, v234, s[0:1] offset:2046
	global_load_ushort v206, v234, s[0:1] offset:2048
	global_load_ushort v207, v234, s[0:1] offset:2050
	global_load_dword v208, v235, s[66:67]
	global_load_dword v209, v235, s[72:73] offset:2048
	global_load_ushort v210, v234, s[0:1] offset:3070
	global_load_ushort v211, v234, s[0:1] offset:3072
	global_load_ushort v212, v234, s[0:1] offset:3074
	global_load_dword v213, v235, s[66:67] offset:2048
	v_lshlrev_b32_e32 v234, 1, v14
	v_add_u32_e32 v234, 0x1000, v234
	v_lshlrev_b32_e32 v235, 2, v14
	v_add_u32_e32 v235, 0x3000, v235
	global_load_dword v214, v235, s[72:73] offset:-4096
	global_load_ushort v215, v234, s[0:1] offset:-2
	global_load_ushort v216, v234, s[0:1]
	global_load_ushort v217, v234, s[0:1] offset:2
	global_load_dword v218, v235, s[66:67] offset:-4096
	global_load_dword v219, v235, s[72:73] offset:-2048
	global_load_ushort v220, v234, s[0:1] offset:1022
	global_load_ushort v221, v234, s[0:1] offset:1024
	global_load_ushort v222, v234, s[0:1] offset:1026
	global_load_dword v223, v235, s[66:67] offset:-2048
	global_load_dword v224, v235, s[72:73]
	global_load_ushort v225, v234, s[0:1] offset:2046
	global_load_ushort v226, v234, s[0:1] offset:2048
	global_load_ushort v227, v234, s[0:1] offset:2050
	global_load_dword v228, v235, s[66:67]
	global_load_dword v229, v235, s[72:73] offset:2048
	global_load_ushort v230, v234, s[0:1] offset:3070
	global_load_ushort v231, v234, s[0:1] offset:3072
	global_load_ushort v232, v234, s[0:1] offset:3074
	global_load_dword v233, v235, s[66:67] offset:2048
	s_waitcnt vmcnt(20)
	v_mov_b32_e32 v10, v190
	s_and_saveexec_b64 s[2:3], vcc
	s_movk_i32 s10, 0x3fff
	s_cbranch_execz .LBB0_2732
	v_mov_b32_e32 v18, v195
	s_nop 0
	v_lshlrev_b32_e32 v18, 16, v18

.LBB0_2734:
	s_or_b64 exec, exec, s[2:3]
	v_add_f32_e32 v6, 0, v6
	v_add_f32_e32 v6, v6, v7
	v_add_f32_e32 v6, v6, v8
	v_add_f32_e32 v6, v6, v9
	v_add_f32_e32 v2, v6, v2
	v_add_f32_e32 v2, v2, v3
	v_add_f32_e32 v2, v2, v4
	v_add_f32_e32 v27, v2, v5
	v_pk_fma_f32 v[2:3], v[58:59], s[92:93], v[58:59] op_sel:[1,0,0] op_sel_hi:[0,1,1]
	v_pk_mul_f32 v[4:5], v[58:59], v[2:3] op_sel:[1,1] op_sel_hi:[0,1] neg_lo:[0,1]
	v_pk_fma_f32 v[4:5], v[58:59], v[2:3], v[4:5] op_sel_hi:[1,0,1]
	s_brev_b32 s6, 28
	v_pk_mul_f32 v[6:7], v[58:59], v[4:5] op_sel:[1,1] op_sel_hi:[0,1] neg_lo:[0,1]
	v_pk_fma_f32 v[6:7], v[58:59], v[4:5], v[6:7] op_sel_hi:[1,0,1]
	v_div_scale_f32 v29, s[4:5], v27, v27, s6
	v_pk_mul_f32 v[8:9], v[58:59], v[6:7] op_sel:[1,1] op_sel_hi:[0,1] neg_lo:[0,1]
	v_pk_fma_f32 v[104:105], v[58:59], v[6:7], v[8:9] op_sel_hi:[1,0,1]
	s_mov_b32 s4, s47
	v_pk_mul_f32 v[8:9], v[58:59], v[104:105] op_sel:[1,1] op_sel_hi:[0,1] neg_lo:[0,1]
	v_pk_fma_f32 v[106:107], v[58:59], v[104:105], v[8:9] op_sel_hi:[1,0,1]
	s_mov_b32 s5, s42
	v_pk_mul_f32 v[8:9], v[58:59], v[106:107] op_sel:[1,1] op_sel_hi:[0,1] neg_lo:[0,1]
	v_pk_fma_f32 v[108:109], v[58:59], v[106:107], v[8:9] op_sel_hi:[1,0,1]
	s_mov_b32 s46, s42
	v_pk_mul_f32 v[8:9], v[58:59], v[108:109] op_sel:[1,1] op_sel_hi:[0,1] neg_lo:[0,1]
	v_pk_fma_f32 v[110:111], v[58:59], v[108:109], v[8:9] op_sel_hi:[1,0,1]
	v_rcp_f32_e32 v31, v29
	v_pk_mul_f32 v[8:9], v[58:59], v[110:111] op_sel:[1,1] op_sel_hi:[0,1] neg_lo:[0,1]
	v_pk_fma_f32 v[112:113], v[58:59], v[110:111], v[8:9] op_sel_hi:[1,0,1]
	v_fma_f32 v33, -v29, v31, 1.0
	v_pk_mul_f32 v[8:9], v[58:59], v[112:113] op_sel:[1,1] op_sel_hi:[0,1] neg_lo:[0,1]
	v_pk_fma_f32 v[114:115], v[58:59], v[112:113], v[8:9] op_sel_hi:[1,0,1]
	v_fmac_f32_e32 v31, v33, v31
	v_pk_mul_f32 v[8:9], v[58:59], v[114:115] op_sel:[1,1] op_sel_hi:[0,1] neg_lo:[0,1]
	v_pk_fma_f32 v[118:119], v[58:59], v[114:115], v[8:9] op_sel_hi:[1,0,1]
	v_div_scale_f32 v33, vcc, s6, v27, s6
	v_pk_mul_f32 v[8:9], v[58:59], v[118:119] op_sel:[1,1] op_sel_hi:[0,1] neg_lo:[0,1]
	v_pk_fma_f32 v[122:123], v[58:59], v[118:119], v[8:9] op_sel_hi:[1,0,1]
	v_mul_f32_e32 v47, v33, v31
	v_pk_mul_f32 v[8:9], v[58:59], v[122:123] op_sel:[1,1] op_sel_hi:[0,1] neg_lo:[0,1]
	v_pk_fma_f32 v[120:121], v[58:59], v[122:123], v[8:9] op_sel_hi:[1,0,1]
	v_fma_f32 v49, -v29, v47, v33
	v_pk_mul_f32 v[8:9], v[58:59], v[120:121] op_sel:[1,1] op_sel_hi:[0,1] neg_lo:[0,1]
	v_pk_fma_f32 v[116:117], v[58:59], v[120:121], v[8:9] op_sel_hi:[1,0,1]
	v_fmac_f32_e32 v47, v49, v31
	v_pk_mul_f32 v[8:9], v[58:59], v[116:117] op_sel:[1,1] op_sel_hi:[0,1] neg_lo:[0,1]
	v_pk_fma_f32 v[124:125], v[58:59], v[116:117], v[8:9] op_sel_hi:[1,0,1]
	v_fma_f32 v29, -v29, v47, v33
	v_pk_mul_f32 v[8:9], v[58:59], v[124:125] op_sel:[1,1] op_sel_hi:[0,1] neg_lo:[0,1]
	v_pk_fma_f32 v[126:127], v[58:59], v[124:125], v[8:9] op_sel_hi:[1,0,1]
	v_div_fmas_f32 v29, v29, v31, v47
	v_pk_mul_f32 v[8:9], v[58:59], v[126:127] op_sel:[1,1] op_sel_hi:[0,1] neg_lo:[0,1]
	v_pk_fma_f32 v[128:129], v[58:59], v[126:127], v[8:9] op_sel_hi:[1,0,1]
	v_div_fixup_f32 v194, v29, v27, s6
	v_pk_mul_f32 v[8:9], v[58:59], v[128:129] op_sel:[1,1] op_sel_hi:[0,1] neg_lo:[0,1]
	v_pk_fma_f32 v[130:131], v[58:59], v[128:129], v[8:9] op_sel_hi:[1,0,1]
	s_xor_b64 s[2:3], s[96:97], -1
	v_pk_mul_f32 v[8:9], v[58:59], v[130:131] op_sel:[1,1] op_sel_hi:[0,1] neg_lo:[0,1]
	v_pk_fma_f32 v[132:133], v[58:59], v[130:131], v[8:9] op_sel_hi:[1,0,1]
	s_mov_b32 s8, 0x3f45e403
	v_pk_mul_f32 v[8:9], v[58:59], v[132:133] op_sel:[1,1] op_sel_hi:[0,1] neg_lo:[0,1]
	v_pk_fma_f32 v[134:135], v[58:59], v[132:133], v[8:9] op_sel_hi:[1,0,1]
	s_mov_b32 s12, 0x3f0e39da
	v_pk_mul_f32 v[8:9], v[58:59], v[134:135] op_sel:[1,1] op_sel_hi:[0,1] neg_lo:[0,1]
	v_pk_fma_f32 v[136:137], v[58:59], v[134:135], v[8:9] op_sel_hi:[1,0,1]
	s_and_b64 vcc, exec, s[2:3]
	v_pk_mul_f32 v[8:9], v[58:59], v[136:137] op_sel:[1,1] op_sel_hi:[0,1] neg_lo:[0,1]
	v_pk_fma_f32 v[138:139], v[58:59], v[136:137], v[8:9] op_sel_hi:[1,0,1]
	s_movk_i32 s45, 0x4000
	v_pk_mul_f32 v[8:9], v[58:59], v[138:139] op_sel:[1,1] op_sel_hi:[0,1] neg_lo:[0,1]
	v_pk_fma_f32 v[140:141], v[58:59], v[138:139], v[8:9] op_sel_hi:[1,0,1]
	s_movk_i32 s50, 0xfc00
	v_pk_mul_f32 v[8:9], v[58:59], v[140:141] op_sel:[1,1] op_sel_hi:[0,1] neg_lo:[0,1]
	v_pk_fma_f32 v[142:143], v[58:59], v[140:141], v[8:9] op_sel_hi:[1,0,1]
	s_movk_i32 s51, 0xfa00
	v_pk_mul_f32 v[8:9], v[58:59], v[142:143] op_sel:[1,1] op_sel_hi:[0,1] neg_lo:[0,1]
	v_pk_fma_f32 v[144:145], v[58:59], v[142:143], v[8:9] op_sel_hi:[1,0,1]
	s_movk_i32 s56, 0xf800
	v_pk_mul_f32 v[8:9], v[58:59], v[144:145] op_sel:[1,1] op_sel_hi:[0,1] neg_lo:[0,1]
	v_pk_fma_f32 v[146:147], v[58:59], v[144:145], v[8:9] op_sel_hi:[1,0,1]
	s_movk_i32 s57, 0xf600
	v_pk_mul_f32 v[8:9], v[58:59], v[146:147] op_sel:[1,1] op_sel_hi:[0,1] neg_lo:[0,1]
	v_pk_fma_f32 v[148:149], v[58:59], v[146:147], v[8:9] op_sel_hi:[1,0,1]
	s_movk_i32 s58, 0xf400
	v_pk_mul_f32 v[8:9], v[58:59], v[148:149] op_sel:[1,1] op_sel_hi:[0,1] neg_lo:[0,1]
	v_pk_fma_f32 v[150:151], v[58:59], v[148:149], v[8:9] op_sel_hi:[1,0,1]
	s_movk_i32 s59, 0xf200
	v_pk_mul_f32 v[8:9], v[58:59], v[150:151] op_sel:[1,1] op_sel_hi:[0,1] neg_lo:[0,1]
	v_pk_fma_f32 v[152:153], v[58:59], v[150:151], v[8:9] op_sel_hi:[1,0,1]
	s_movk_i32 s60, 0xf000
	v_pk_mul_f32 v[8:9], v[58:59], v[152:153] op_sel:[1,1] op_sel_hi:[0,1] neg_lo:[0,1]
	v_pk_fma_f32 v[154:155], v[58:59], v[152:153], v[8:9] op_sel_hi:[1,0,1]
	s_movk_i32 s62, 0xee00
	v_pk_mul_f32 v[8:9], v[58:59], v[154:155] op_sel:[1,1] op_sel_hi:[0,1] neg_lo:[0,1]
	v_pk_fma_f32 v[156:157], v[58:59], v[154:155], v[8:9] op_sel_hi:[1,0,1]
	s_movk_i32 s63, 0xec00
	v_pk_mul_f32 v[8:9], v[58:59], v[156:157] op_sel:[1,1] op_sel_hi:[0,1] neg_lo:[0,1]
	v_pk_fma_f32 v[8:9], v[58:59], v[156:157], v[8:9] op_sel_hi:[1,0,1]
	s_nop 0
	v_pk_mul_f32 v[58:59], v[102:103], v[8:9] op_sel:[1,1] op_sel_hi:[0,1] neg_hi:[1,0]
	s_movk_i32 s64, 0xea00
	v_pk_fma_f32 v[8:9], v[102:103], v[8:9], v[58:59] op_sel_hi:[1,0,1]
	v_pk_mul_f32 v[58:59], v[100:101], v[156:157] op_sel:[1,1] op_sel_hi:[0,1] neg_hi:[1,0]
	s_movk_i32 s65, 0xe800
	v_pk_fma_f32 v[58:59], v[100:101], v[156:157], v[58:59] op_sel_hi:[1,0,1]
	v_pk_mul_f32 v[100:101], v[60:61], v[154:155] op_sel:[1,1] op_sel_hi:[0,1] neg_hi:[1,0]
	s_mov_b32 s9, 0xbf226799
	v_pk_fma_f32 v[60:61], v[60:61], v[154:155], v[100:101] op_sel_hi:[1,0,1]
	v_pk_mul_f32 v[100:101], v[62:63], v[152:153] op_sel:[1,1] op_sel_hi:[0,1] neg_hi:[1,0]
	s_mov_b32 s13, 0xbf54db31
	v_pk_fma_f32 v[62:63], v[62:63], v[152:153], v[100:101] op_sel_hi:[1,0,1]
	v_pk_mul_f32 v[100:101], v[66:67], v[150:151] op_sel:[1,1] op_sel_hi:[0,1] neg_hi:[1,0]
	s_movk_i32 s11, 0xfe00
	v_pk_fma_f32 v[66:67], v[66:67], v[150:151], v[100:101] op_sel_hi:[1,0,1]
	v_pk_mul_f32 v[100:101], v[68:69], v[148:149] op_sel:[1,1] op_sel_hi:[0,1] neg_hi:[1,0]
	s_nop 0
	v_pk_fma_f32 v[68:69], v[68:69], v[148:149], v[100:101] op_sel_hi:[1,0,1]
	v_pk_mul_f32 v[100:101], v[70:71], v[146:147] op_sel:[1,1] op_sel_hi:[0,1] neg_hi:[1,0]
	s_nop 0
	v_pk_fma_f32 v[70:71], v[70:71], v[146:147], v[100:101] op_sel_hi:[1,0,1]
	v_pk_mul_f32 v[100:101], v[72:73], v[144:145] op_sel:[1,1] op_sel_hi:[0,1] neg_hi:[1,0]
	s_nop 0
	v_pk_fma_f32 v[72:73], v[72:73], v[144:145], v[100:101] op_sel_hi:[1,0,1]
	v_pk_mul_f32 v[100:101], v[90:91], v[142:143] op_sel:[1,1] op_sel_hi:[0,1] neg_hi:[1,0]
	s_nop 0
	v_pk_fma_f32 v[90:91], v[90:91], v[142:143], v[100:101] op_sel_hi:[1,0,1]
	v_pk_mul_f32 v[100:101], v[94:95], v[140:141] op_sel:[1,1] op_sel_hi:[0,1] neg_hi:[1,0]
	s_nop 0
	v_pk_fma_f32 v[94:95], v[94:95], v[140:141], v[100:101] op_sel_hi:[1,0,1]
	v_pk_mul_f32 v[100:101], v[98:99], v[138:139] op_sel:[1,1] op_sel_hi:[0,1] neg_hi:[1,0]
	s_nop 0
	v_pk_fma_f32 v[144:145], v[98:99], v[138:139], v[100:101] op_sel_hi:[1,0,1]
	v_pk_mul_f32 v[98:99], v[96:97], v[136:137] op_sel:[1,1] op_sel_hi:[0,1] neg_hi:[1,0]
	s_nop 0
	v_pk_fma_f32 v[138:139], v[96:97], v[136:137], v[98:99] op_sel_hi:[1,0,1]
	v_pk_mul_f32 v[96:97], v[92:93], v[134:135] op_sel:[1,1] op_sel_hi:[0,1] neg_hi:[1,0]
	s_nop 0
	v_pk_fma_f32 v[136:137], v[92:93], v[134:135], v[96:97] op_sel_hi:[1,0,1]
	v_pk_mul_f32 v[92:93], v[88:89], v[132:133] op_sel:[1,1] op_sel_hi:[0,1] neg_hi:[1,0]
	s_nop 0
	v_pk_fma_f32 v[134:135], v[88:89], v[132:133], v[92:93] op_sel_hi:[1,0,1]
	v_pk_mul_f32 v[88:89], v[86:87], v[130:131] op_sel:[1,1] op_sel_hi:[0,1] neg_hi:[1,0]
	s_nop 0
	v_pk_fma_f32 v[132:133], v[86:87], v[130:131], v[88:89] op_sel_hi:[1,0,1]
	v_pk_mul_f32 v[86:87], v[84:85], v[128:129] op_sel:[1,1] op_sel_hi:[0,1] neg_hi:[1,0]
	s_nop 0
	v_pk_fma_f32 v[130:131], v[84:85], v[128:129], v[86:87] op_sel_hi:[1,0,1]
	v_pk_mul_f32 v[84:85], v[82:83], v[126:127] op_sel:[1,1] op_sel_hi:[0,1] neg_hi:[1,0]
	v_mov_b32_e32 v86, v19
	v_pk_fma_f32 v[92:93], v[82:83], v[126:127], v[84:85] op_sel_hi:[1,0,1]
	v_pk_mul_f32 v[82:83], v[80:81], v[124:125] op_sel:[1,1] op_sel_hi:[0,1] neg_hi:[1,0]
	v_pk_mul_f32 v[86:87], v[86:87], s[4:5] op_sel_hi:[0,1] neg_lo:[1,0]
	v_pk_fma_f32 v[96:97], v[80:81], v[124:125], v[82:83] op_sel_hi:[1,0,1]
	v_pk_mul_f32 v[80:81], v[78:79], v[116:117] op_sel:[1,1] op_sel_hi:[0,1] neg_hi:[1,0]
	v_pk_add_f32 v[88:89], v[96:97], v[58:59]
	v_pk_fma_f32 v[116:117], v[78:79], v[116:117], v[80:81] op_sel_hi:[1,0,1]
	v_pk_mul_f32 v[78:79], v[76:77], v[120:121] op_sel:[1,1] op_sel_hi:[0,1] neg_hi:[1,0]
	v_pk_fma_f32 v[86:87], v[16:17], s[46:47], v[86:87] op_sel_hi:[0,1,1]
	v_pk_fma_f32 v[120:121], v[76:77], v[120:121], v[78:79] op_sel_hi:[1,0,1]
	v_pk_mul_f32 v[76:77], v[74:75], v[122:123] op_sel:[1,1] op_sel_hi:[0,1] neg_hi:[1,0]
	v_pk_add_f32 v[78:79], v[92:93], v[8:9]
	v_pk_fma_f32 v[122:123], v[74:75], v[122:123], v[76:77] op_sel_hi:[1,0,1]
	v_pk_mul_f32 v[74:75], v[64:65], v[118:119] op_sel:[1,1] op_sel_hi:[0,1] neg_hi:[1,0]
	s_mov_b64 s[4:5], -1
	v_pk_fma_f32 v[124:125], v[64:65], v[118:119], v[74:75] op_sel_hi:[1,0,1]
	v_pk_mul_f32 v[64:65], v[56:57], v[114:115] op_sel:[1,1] op_sel_hi:[0,1] neg_hi:[1,0]
	s_nop 0
	v_pk_fma_f32 v[126:127], v[56:57], v[114:115], v[64:65] op_sel_hi:[1,0,1]
	v_pk_mul_f32 v[56:57], v[54:55], v[112:113] op_sel:[1,1] op_sel_hi:[0,1] neg_hi:[1,0]
	v_pk_add_f32 v[118:119], v[126:127], v[70:71]
	v_pk_fma_f32 v[128:129], v[54:55], v[112:113], v[56:57] op_sel_hi:[1,0,1]
	v_pk_mul_f32 v[54:55], v[52:53], v[110:111] op_sel:[1,1] op_sel_hi:[0,1] neg_hi:[1,0]
	v_pk_add_f32 v[114:115], v[128:129], v[72:73]
	v_pk_fma_f32 v[140:141], v[52:53], v[110:111], v[54:55] op_sel_hi:[1,0,1]
	v_pk_mul_f32 v[52:53], v[50:51], v[108:109] op_sel:[1,1] op_sel_hi:[0,1] neg_hi:[1,0]
	v_pk_add_f32 v[64:65], v[140:141], v[90:91]
	v_pk_fma_f32 v[142:143], v[50:51], v[108:109], v[52:53] op_sel_hi:[1,0,1]
	v_pk_mul_f32 v[50:51], v[44:45], v[106:107] op_sel:[1,1] op_sel_hi:[0,1] neg_hi:[1,0]
	v_pk_add_f32 v[74:75], v[142:143], v[94:95]
	v_pk_fma_f32 v[146:147], v[44:45], v[106:107], v[50:51] op_sel_hi:[1,0,1]
	v_pk_mul_f32 v[44:45], v[42:43], v[104:105] op_sel:[1,1] op_sel_hi:[0,1] neg_hi:[1,0]
	v_pk_add_f32 v[76:77], v[146:147], v[144:145]
	v_pk_fma_f32 v[148:149], v[42:43], v[104:105], v[44:45] op_sel_hi:[1,0,1]
	v_pk_mul_f32 v[42:43], v[40:41], v[6:7] op_sel:[1,1] op_sel_hi:[0,1] neg_hi:[1,0]
	v_pk_add_f32 v[80:81], v[148:149], v[138:139]
	v_pk_fma_f32 v[150:151], v[40:41], v[6:7], v[42:43] op_sel_hi:[1,0,1]
	v_pk_mul_f32 v[6:7], v[38:39], v[4:5] op_sel:[1,1] op_sel_hi:[0,1] neg_hi:[1,0]
	v_pk_add_f32 v[104:105], v[150:151], v[136:137]
	v_pk_fma_f32 v[152:153], v[38:39], v[4:5], v[6:7] op_sel_hi:[1,0,1]
	v_pk_mul_f32 v[4:5], v[2:3], v[36:37] op_sel:[1,1] op_sel_hi:[1,0] neg_hi:[0,1]
	v_pk_add_f32 v[102:103], v[152:153], v[134:135]
	v_pk_fma_f32 v[154:155], v[36:37], v[2:3], v[4:5] op_sel_hi:[1,0,1]
	v_pk_fma_f32 v[156:157], v[34:35], 0, v[34:35] op_sel:[1,0,0] op_sel_hi:[0,0,1] neg_hi:[1,0,0]
	v_pk_add_f32 v[100:101], v[154:155], v[132:133]
	v_pk_add_f32 v[98:99], v[156:157], v[130:131]
	v_pk_add_f32 v[112:113], v[124:125], v[68:69]
	v_pk_add_f32 v[110:111], v[122:123], v[66:67]
	v_pk_add_f32 v[106:107], v[120:121], v[62:63]
	v_pk_add_f32 v[108:109], v[116:117], v[60:61]
	v_pk_add_f32 v[40:41], v[98:99], v[114:115]
	v_pk_add_f32 v[42:43], v[100:101], v[118:119]
	v_pk_add_f32 v[36:37], v[102:103], v[112:113]
	v_pk_add_f32 v[34:35], v[104:105], v[110:111]
	v_pk_add_f32 v[82:83], v[80:81], v[106:107]
	v_pk_add_f32 v[84:85], v[76:77], v[108:109]
	v_pk_add_f32 v[44:45], v[74:75], v[88:89]
	v_pk_add_f32 v[38:39], v[64:65], v[78:79]
	v_pk_add_f32 v[50:51], v[40:41], v[82:83]
	v_pk_add_f32 v[52:53], v[42:43], v[84:85]
	v_pk_add_f32 v[54:55], v[36:37], v[44:45]
	v_pk_add_f32 v[56:57], v[34:35], v[38:39]
	v_pk_add_f32 v[4:5], v[50:51], v[54:55]
	v_pk_add_f32 v[6:7], v[52:53], v[56:57]
	s_nop 0
	v_pk_add_f32 v[2:3], v[4:5], v[6:7]
	s_nop 0
	v_pk_mul_f32 v[2:3], v[86:87], v[2:3]
	v_lshl_add_u64 v[86:87], v[14:15], 1, s[54:55]
	s_nop 0
	v_add_f32_e32 v2, v10, v2
	v_add_f32_e32 v10, v3, v2
	s_nop 0
	v_lshlrev_b32_e32 v2, 16, v25
	v_mul_f32_e32 v2, v191, v2
	v_fmac_f32_e32 v2, v189, v18
	v_fmac_f32_e32 v2, v192, v17
	v_add_f32_e32 v17, v193, v2
	v_lshl_add_u64 v[2:3], v[14:15], 2, s[66:67]
	v_mov_b32_e32 v18, v198
	s_nop 0
	v_mul_f32_e32 v18, v13, v18
	v_fmac_f32_e32 v18, v194, v10
	v_mul_f32_e32 v10, v17, v18
	s_cbranch_vccz .LBB0_2736
	v_bfe_u32 v15, v10, 16, 1
	v_add3_u32 v15, v10, v15, s33
	global_store_short_d16_hi v[86:87], v15, off
	s_mov_b64 s[4:5], 0

.LBB0_2742:
	s_or_b64 exec, exec, s[4:5]
	v_pk_add_f32 v[134:135], v[152:153], v[134:135] neg_lo:[0,1] neg_hi:[0,1]
	v_pk_add_f32 v[144:145], v[146:147], v[144:145] neg_lo:[0,1] neg_hi:[0,1]
	s_nop 0
	v_pk_mul_f32 v[152:153], v[30:31], v[134:135] op_sel:[0,1] op_sel_hi:[0,0] neg_lo:[0,1]
	v_pk_fma_f32 v[134:135], v[32:33], v[134:135], v[152:153] op_sel_hi:[0,1,1]
	v_mov_b32_e32 v33, v203
	v_pk_add_f32 v[138:139], v[148:149], v[138:139] neg_lo:[0,1] neg_hi:[0,1]
	v_pk_mul_f32 v[146:147], v[28:29], v[144:145] op_sel:[0,1] op_sel_hi:[0,0] neg_lo:[0,1]
	v_pk_add_f32 v[72:73], v[128:129], v[72:73] neg_lo:[0,1] neg_hi:[0,1]
	v_pk_add_f32 v[70:71], v[126:127], v[70:71] neg_lo:[0,1] neg_hi:[0,1]
	v_pk_fma_f32 v[144:145], v[48:49], v[144:145], v[146:147] op_sel_hi:[0,1,1]
	v_xor_b32_e32 v146, 0x80000000, v73
	v_mov_b32_e32 v147, v72
	v_pk_mul_f32 v[148:149], v[46:47], v[138:139] op_sel:[0,1] op_sel_hi:[0,0] neg_lo:[0,1]
	v_pk_mul_f32 v[72:73], v[24:25], v[70:71] op_sel:[0,1] op_sel_hi:[0,0] neg_lo:[0,1]
	v_pk_add_f32 v[68:69], v[124:125], v[68:69] neg_lo:[0,1] neg_hi:[0,1]
	v_pk_fma_f32 v[138:139], v[46:47], v[138:139], v[148:149] op_sel_hi:[0,1,1]
	v_pk_fma_f32 v[148:149], v[26:27], v[70:71], v[72:73] op_sel_hi:[0,1,1] neg_lo:[1,0,0] neg_hi:[1,0,0]
	v_pk_add_f32 v[136:137], v[150:151], v[136:137] neg_lo:[0,1] neg_hi:[0,1]
	v_pk_add_f32 v[66:67], v[122:123], v[66:67] neg_lo:[0,1] neg_hi:[0,1]
	v_pk_mul_f32 v[150:151], v[48:49], v[136:137] op_sel:[0,1] op_sel_hi:[0,0] neg_lo:[0,1]
	v_pk_add_f32 v[62:63], v[120:121], v[62:63] neg_lo:[0,1] neg_hi:[0,1]
	v_pk_fma_f32 v[136:137], v[28:29], v[136:137], v[150:151] op_sel_hi:[0,1,1]
	v_pk_add_f32 v[132:133], v[154:155], v[132:133] neg_lo:[0,1] neg_hi:[0,1]
	v_pk_add_f32 v[60:61], v[116:117], v[60:61] neg_lo:[0,1] neg_hi:[0,1]
	v_pk_mul_f32 v[154:155], v[26:27], v[132:133] op_sel:[0,1] op_sel_hi:[0,0] neg_lo:[0,1]
	v_pk_add_f32 v[94:95], v[142:143], v[94:95] neg_lo:[0,1] neg_hi:[0,1]
	v_pk_fma_f32 v[132:133], v[24:25], v[132:133], v[154:155] op_sel_hi:[0,1,1]
	v_pk_add_f32 v[90:91], v[140:141], v[90:91] neg_lo:[0,1] neg_hi:[0,1]
	v_pk_add_f32 v[8:9], v[92:93], v[8:9] neg_lo:[0,1] neg_hi:[0,1]
	v_pk_add_f32 v[130:131], v[156:157], v[130:131] neg_lo:[0,1] neg_hi:[0,1]
	v_pk_add_f32 v[92:93], v[132:133], v[148:149]
	v_xor_b32_e32 v18, 0x80000000, v19
	s_mov_b32 s4, s69
	s_mov_b32 s5, s68
	v_mov_b32_e32 v17, v16
	s_andn2_b64 vcc, exec, s[2:3]
	s_nop 0
	v_pk_mul_f32 v[70:71], v[32:33], v[68:69] op_sel:[0,1] op_sel_hi:[0,0] neg_lo:[0,1]
	v_pk_fma_f32 v[124:125], v[30:31], v[68:69], v[70:71] op_sel_hi:[0,1,1] neg_lo:[1,0,0] neg_hi:[1,0,0]
	v_pk_mul_f32 v[68:69], v[28:29], v[66:67] op_sel:[0,1] op_sel_hi:[0,0] neg_lo:[0,1]
	v_pk_fma_f32 v[150:151], v[48:49], v[66:67], v[68:69] op_sel_hi:[0,1,1] neg_lo:[1,0,0] neg_hi:[1,0,0]
	v_pk_mul_f32 v[66:67], v[46:47], v[62:63] op_sel:[0,1] op_sel_hi:[0,0] neg_lo:[0,1]
	v_pk_fma_f32 v[152:153], v[46:47], v[62:63], v[66:67] op_sel_hi:[0,1,1] neg_lo:[1,0,0] neg_hi:[1,0,0]
	v_xor_b32_e32 v62, 0x80000000, v61
	v_mov_b32_e32 v63, v60
	v_pk_mul_f32 v[48:49], v[48:49], v[62:63] op_sel_hi:[0,1]
	v_pk_fma_f32 v[154:155], v[28:29], v[60:61], v[48:49] op_sel_hi:[0,1,1] neg_lo:[1,0,0] neg_hi:[1,0,0]
	v_pk_add_f32 v[28:29], v[96:97], v[58:59] neg_lo:[0,1] neg_hi:[0,1]
	v_pk_mul_f32 v[142:143], v[32:33], v[94:95] op_sel:[0,1] op_sel_hi:[0,0] neg_lo:[0,1]
	v_pk_fma_f32 v[142:143], v[30:31], v[94:95], v[142:143] op_sel_hi:[0,1,1]
	v_pk_mul_f32 v[48:49], v[30:31], v[28:29] op_sel:[0,1] op_sel_hi:[0,0] neg_lo:[0,1]
	v_pk_mul_f32 v[94:95], v[24:25], v[90:91] op_sel:[0,1] op_sel_hi:[0,0] neg_lo:[0,1]
	v_pk_fma_f32 v[156:157], v[32:33], v[28:29], v[48:49] op_sel_hi:[0,1,1] neg_lo:[1,0,0] neg_hi:[1,0,0]
	v_pk_fma_f32 v[140:141], v[26:27], v[90:91], v[94:95] op_sel_hi:[0,1,1]
	v_pk_mul_f32 v[26:27], v[26:27], v[8:9] op_sel:[0,1] op_sel_hi:[0,0] neg_lo:[0,1]
	v_pk_fma_f32 v[158:159], v[24:25], v[8:9], v[26:27] op_sel_hi:[0,1,1] neg_lo:[1,0,0] neg_hi:[1,0,0]
	v_pk_add_f32 v[90:91], v[130:131], v[146:147]
	v_pk_add_f32 v[94:95], v[134:135], v[124:125]
	v_pk_add_f32 v[96:97], v[136:137], v[150:151]
	v_pk_add_f32 v[126:127], v[138:139], v[152:153]
	v_pk_add_f32 v[128:129], v[144:145], v[154:155]
	v_pk_add_f32 v[122:123], v[142:143], v[156:157]
	v_pk_add_f32 v[116:117], v[140:141], v[158:159]
	v_pk_add_f32 v[66:67], v[90:91], v[126:127]
	v_pk_add_f32 v[68:69], v[92:93], v[128:129]
	v_pk_add_f32 v[70:71], v[94:95], v[122:123]
	v_pk_add_f32 v[72:73], v[96:97], v[116:117]
	v_pk_add_f32 v[26:27], v[66:67], v[70:71]
	v_pk_add_f32 v[28:29], v[68:69], v[72:73]
	v_pk_mul_f32 v[48:49], v[18:19], s[4:5]
	v_pk_add_f32 v[8:9], v[26:27], v[28:29]
	v_pk_fma_f32 v[48:49], v[16:17], s[68:69], v[48:49]
	s_nop 0
	v_pk_mul_f32 v[8:9], v[48:49], v[8:9]
	s_nop 0
	v_add_f32_e32 v8, v8, v25
	v_add_f32_e32 v8, v9, v8
	v_lshlrev_b32_e32 v9, 16, v31
	v_mul_f32_e32 v9, v191, v9
	v_fmac_f32_e32 v9, v189, v10
	v_fmac_f32_e32 v9, v192, v15
	v_mul_f32_e32 v10, v13, v33
	v_add_f32_e32 v9, v193, v9
	v_fmac_f32_e32 v10, v194, v8
	v_mul_f32_e32 v8, v9, v10
	v_cndmask_b32_e64 v9, 0, 1, s[2:3]
	v_cmp_ne_u32_e64 s[4:5], 1, v9
	s_mov_b64 s[2:3], -1
	s_cbranch_vccnz .LBB0_2744
	v_bfe_u32 v9, v8, 16, 1
	v_add3_u32 v9, v8, v9, s33
	s_mov_b64 s[2:3], 0
	global_store_short_d16_hi v[86:87], v9, off offset:1024

.LBB0_2750:
	s_or_b64 exec, exec, s[2:3]
	v_pk_add_f32 v[8:9], v[100:101], v[118:119] neg_lo:[0,1] neg_hi:[0,1]
	v_mov_b32_e32 v31, v30
	v_mov_b32_e32 v33, v32
	v_pk_mul_f32 v[24:25], v[30:31], v[8:9] op_sel:[0,1] op_sel_hi:[1,0] neg_lo:[0,1]
	v_mov_b32_e32 v47, v46
	v_pk_fma_f32 v[100:101], v[32:33], v[8:9], v[24:25]
	v_pk_add_f32 v[8:9], v[102:103], v[112:113] neg_lo:[0,1] neg_hi:[0,1]
	v_xor_b32_e32 v162, 0x80000000, v30
	v_pk_mul_f32 v[24:25], v[46:47], v[8:9] op_sel:[0,1] op_sel_hi:[1,0] neg_lo:[0,1]
	v_mov_b32_e32 v163, v162
	v_pk_fma_f32 v[102:103], v[46:47], v[8:9], v[24:25]
	v_pk_add_f32 v[8:9], v[104:105], v[110:111] neg_lo:[0,1] neg_hi:[0,1]
	v_xor_b32_e32 v48, 0x80000000, v46
	v_pk_mul_f32 v[24:25], v[32:33], v[8:9] op_sel:[0,1] op_sel_hi:[1,0] neg_lo:[0,1]
	v_mov_b32_e32 v49, v48
	v_pk_fma_f32 v[104:105], v[30:31], v[8:9], v[24:25]
	v_pk_add_f32 v[8:9], v[80:81], v[106:107] neg_lo:[0,1] neg_hi:[0,1]
	v_xor_b32_e32 v160, 0x80000000, v32
	v_xor_b32_e32 v106, 0x80000000, v9
	v_mov_b32_e32 v107, v8
	v_pk_add_f32 v[8:9], v[76:77], v[108:109] neg_lo:[0,1] neg_hi:[0,1]
	v_mov_b32_e32 v161, v160
	v_pk_mul_f32 v[24:25], v[32:33], v[8:9] op_sel:[0,1] op_sel_hi:[1,0] neg_lo:[0,1]
	v_pk_add_f32 v[98:99], v[98:99], v[114:115] neg_lo:[0,1] neg_hi:[0,1]
	v_pk_fma_f32 v[108:109], v[162:163], v[8:9], v[24:25]
	v_pk_add_f32 v[8:9], v[74:75], v[88:89] neg_lo:[0,1] neg_hi:[0,1]
	v_pk_add_f32 v[58:59], v[98:99], v[106:107]
	v_pk_mul_f32 v[24:25], v[46:47], v[8:9] op_sel:[0,1] op_sel_hi:[1,0] neg_lo:[0,1]
	v_pk_add_f32 v[60:61], v[100:101], v[108:109]
	v_pk_fma_f32 v[110:111], v[48:49], v[8:9], v[24:25]
	v_pk_add_f32 v[8:9], v[64:65], v[78:79] neg_lo:[0,1] neg_hi:[0,1]
	v_pk_add_f32 v[62:63], v[102:103], v[110:111]
	v_pk_mul_f32 v[24:25], v[30:31], v[8:9] op_sel:[0,1] op_sel_hi:[1,0] neg_lo:[0,1]
	s_mov_b32 s2, s71
	v_pk_fma_f32 v[112:113], v[160:161], v[8:9], v[24:25]
	s_mov_b32 s3, s70
	v_pk_add_f32 v[64:65], v[104:105], v[112:113]
	v_pk_add_f32 v[8:9], v[58:59], v[62:63]
	v_pk_add_f32 v[24:25], v[60:61], v[64:65]
	v_pk_mul_f32 v[76:77], v[18:19], s[2:3]
	v_pk_add_f32 v[74:75], v[8:9], v[24:25]
	v_pk_fma_f32 v[76:77], v[16:17], s[70:71], v[76:77]
	s_mov_b64 s[2:3], -1
	v_pk_mul_f32 v[74:75], v[76:77], v[74:75]
	s_nop 0
	v_add_f32_e32 v74, v74, v120
	v_add_f32_e32 v76, v75, v74
	s_nop 0
	v_lshlrev_b32_e32 v74, 16, v121
	v_mul_f32_e32 v74, v191, v74
	v_fmac_f32_e32 v74, v189, v10
	v_fmac_f32_e32 v74, v192, v15
	v_add_f32_e32 v10, v193, v74
	v_add_co_u32_e32 v74, vcc, 0x1000, v2
	s_nop 1
	v_addc_co_u32_e32 v75, vcc, 0, v3, vcc
	v_mov_b32_e32 v15, v208
	s_and_b64 vcc, exec, s[4:5]
	s_nop 0
	v_mul_f32_e32 v15, v13, v15
	v_fmac_f32_e32 v15, v194, v76
	v_mul_f32_e32 v10, v10, v15
	s_cbranch_vccnz .LBB0_2752
	v_bfe_u32 v15, v10, 16, 1
	v_add3_u32 v15, v10, v15, s33
	s_mov_b64 s[2:3], 0
	global_store_short_d16_hi v[86:87], v15, off offset:2048

.LBB0_2758:
	s_or_b64 exec, exec, s[2:3]
	v_pk_add_f32 v[74:75], v[132:133], v[148:149] neg_lo:[0,1] neg_hi:[0,1]
	v_pk_add_f32 v[114:115], v[130:131], v[146:147] neg_lo:[0,1] neg_hi:[0,1]
	v_pk_mul_f32 v[76:77], v[30:31], v[74:75] op_sel:[0,1] op_sel_hi:[1,0] neg_lo:[0,1]
	s_mov_b32 s2, s41
	v_pk_fma_f32 v[118:119], v[32:33], v[74:75], v[76:77]
	v_pk_add_f32 v[74:75], v[134:135], v[124:125] neg_lo:[0,1] neg_hi:[0,1]
	s_mov_b32 s3, s40
	v_pk_mul_f32 v[76:77], v[46:47], v[74:75] op_sel:[0,1] op_sel_hi:[1,0] neg_lo:[0,1]
	s_nop 0
	v_pk_fma_f32 v[120:121], v[46:47], v[74:75], v[76:77]
	v_pk_add_f32 v[74:75], v[136:137], v[150:151] neg_lo:[0,1] neg_hi:[0,1]
	s_nop 0
	v_pk_mul_f32 v[76:77], v[32:33], v[74:75] op_sel:[0,1] op_sel_hi:[1,0] neg_lo:[0,1]
	s_nop 0
	v_pk_fma_f32 v[124:125], v[30:31], v[74:75], v[76:77]
	v_pk_add_f32 v[74:75], v[138:139], v[152:153] neg_lo:[0,1] neg_hi:[0,1]
	s_nop 0
	v_xor_b32_e32 v130, 0x80000000, v75
	v_mov_b32_e32 v131, v74
	v_pk_add_f32 v[74:75], v[144:145], v[154:155] neg_lo:[0,1] neg_hi:[0,1]
	s_nop 0
	v_pk_mul_f32 v[32:33], v[32:33], v[74:75] op_sel:[0,1] op_sel_hi:[1,0] neg_lo:[0,1]
	s_nop 0
	v_pk_fma_f32 v[132:133], v[162:163], v[74:75], v[32:33]
	v_pk_add_f32 v[32:33], v[142:143], v[156:157] neg_lo:[0,1] neg_hi:[0,1]
	v_pk_add_f32 v[76:77], v[118:119], v[132:133]
	v_pk_mul_f32 v[74:75], v[46:47], v[32:33] op_sel:[0,1] op_sel_hi:[1,0] neg_lo:[0,1]
	s_nop 0
	v_pk_fma_f32 v[134:135], v[48:49], v[32:33], v[74:75]
	v_pk_add_f32 v[32:33], v[140:141], v[158:159] neg_lo:[0,1] neg_hi:[0,1]
	v_pk_add_f32 v[78:79], v[120:121], v[134:135]
	v_pk_mul_f32 v[30:31], v[30:31], v[32:33] op_sel:[0,1] op_sel_hi:[1,0] neg_lo:[0,1]
	v_pk_add_f32 v[74:75], v[114:115], v[130:131]
	v_pk_fma_f32 v[136:137], v[160:161], v[32:33], v[30:31]
	v_pk_add_f32 v[30:31], v[74:75], v[78:79]
	v_pk_add_f32 v[80:81], v[124:125], v[136:137]
	v_pk_mul_f32 v[140:141], v[18:19], s[2:3]
	v_pk_add_f32 v[32:33], v[76:77], v[80:81]
	v_pk_fma_f32 v[140:141], v[16:17], s[40:41], v[140:141]
	v_pk_add_f32 v[138:139], v[30:31], v[32:33]
	s_mov_b64 s[2:3], -1
	v_pk_mul_f32 v[138:139], v[140:141], v[138:139]
	s_nop 0
	v_add_f32_e32 v88, v138, v88
	v_add_f32_e32 v138, v139, v88
	s_nop 0
	v_lshlrev_b32_e32 v88, 16, v89
	v_mul_f32_e32 v88, v191, v88
	v_fmac_f32_e32 v88, v189, v10
	v_fmac_f32_e32 v88, v192, v15
	v_add_f32_e32 v10, v193, v88
	v_add_co_u32_e32 v88, vcc, 0x1000, v2
	s_nop 1
	v_addc_co_u32_e32 v89, vcc, 0, v3, vcc
	v_mov_b32_e32 v15, v213
	s_and_b64 vcc, exec, s[4:5]
	s_nop 0
	v_mul_f32_e32 v15, v13, v15
	v_fmac_f32_e32 v15, v194, v138
	v_mul_f32_e32 v10, v10, v15
	s_cbranch_vccnz .LBB0_2760
	v_bfe_u32 v15, v10, 16, 1
	v_add3_u32 v15, v10, v15, s33
	s_mov_b64 s[2:3], 0
	global_store_short_d16_hi v[86:87], v15, off offset:3072

.LBB0_2766:
	s_or_b64 exec, exec, s[2:3]
	v_pk_add_f32 v[82:83], v[40:41], v[82:83] neg_lo:[0,1] neg_hi:[0,1]
	v_pk_add_f32 v[40:41], v[42:43], v[84:85] neg_lo:[0,1] neg_hi:[0,1]
	v_pk_add_f32 v[36:37], v[36:37], v[44:45] neg_lo:[0,1] neg_hi:[0,1]
	v_pk_add_f32 v[34:35], v[34:35], v[38:39] neg_lo:[0,1] neg_hi:[0,1]
	v_xor_b32_e32 v86, 0x80000000, v37
	v_mov_b32_e32 v87, v36
	v_pk_mul_f32 v[42:43], v[46:47], v[40:41] op_sel:[0,1] op_sel_hi:[1,0] neg_lo:[0,1]
	v_pk_mul_f32 v[36:37], v[46:47], v[34:35] op_sel:[0,1] op_sel_hi:[1,0] neg_lo:[0,1]
	v_pk_fma_f32 v[84:85], v[46:47], v[40:41], v[42:43]
	v_pk_fma_f32 v[88:89], v[48:49], v[34:35], v[36:37]
	s_mov_b32 s2, s95
	s_mov_b32 s3, s94
	v_pk_add_f32 v[34:35], v[82:83], v[86:87]
	v_pk_add_f32 v[36:37], v[84:85], v[88:89]
	v_pk_mul_f32 v[40:41], v[18:19], s[2:3]
	v_pk_add_f32 v[38:39], v[34:35], v[36:37]
	v_pk_fma_f32 v[40:41], v[16:17], s[94:95], v[40:41]
	s_mov_b64 s[2:3], -1
	v_pk_mul_f32 v[38:39], v[40:41], v[38:39]
	s_nop 0
	v_add_f32_e32 v10, v38, v10
	s_nop 0
	v_lshlrev_b32_e32 v38, 16, v141
	v_mul_f32_e32 v38, v191, v38
	v_fmac_f32_e32 v38, v189, v140
	v_fmac_f32_e32 v38, v192, v15
	v_add_f32_e32 v15, v193, v38
	v_add_co_u32_e32 v38, vcc, 0x2000, v2
	v_add_f32_e32 v10, v39, v10
	s_nop 0
	v_addc_co_u32_e32 v39, vcc, 0, v3, vcc
	v_mov_b32_e32 v38, v218
	s_and_b64 vcc, exec, s[4:5]
	s_nop 0
	v_mul_f32_e32 v38, v13, v38
	v_fmac_f32_e32 v38, v194, v10
	v_mul_f32_e32 v10, v15, v38
	s_cbranch_vccnz .LBB0_2768
	v_bfe_u32 v15, v10, 16, 1
	v_add3_u32 v15, v10, v15, s33
	v_lshl_add_u64 v[38:39], v[138:139], 1, s[54:55]
	s_mov_b64 s[2:3], 0
	global_store_short_d16_hi v[38:39], v15, off

.LBB0_2774:
	s_or_b64 exec, exec, s[2:3]
	s_nop 0
	v_lshlrev_b32_e32 v45, 16, v45
	v_mul_f32_e32 v45, v191, v45
	v_fmac_f32_e32 v45, v189, v44
	v_fmac_f32_e32 v45, v192, v15
	v_add_co_u32_e32 v44, vcc, 0x2000, v2
	v_add_f32_e32 v15, v193, v45
	s_nop 0
	v_addc_co_u32_e32 v45, vcc, 0, v3, vcc
	v_mov_b32_e32 v44, v223
	v_pk_add_f32 v[38:39], v[92:93], v[128:129] neg_lo:[0,1] neg_hi:[0,1]
	v_pk_add_f32 v[90:91], v[90:91], v[126:127] neg_lo:[0,1] neg_hi:[0,1]
	v_pk_mul_f32 v[40:41], v[46:47], v[38:39] op_sel:[0,1] op_sel_hi:[1,0] neg_lo:[0,1]
	s_mov_b32 s2, s79
	v_pk_fma_f32 v[92:93], v[46:47], v[38:39], v[40:41]
	v_pk_add_f32 v[38:39], v[94:95], v[122:123] neg_lo:[0,1] neg_hi:[0,1]
	s_mov_b32 s3, s78
	v_xor_b32_e32 v94, 0x80000000, v39
	v_mov_b32_e32 v95, v38
	v_pk_add_f32 v[38:39], v[96:97], v[116:117] neg_lo:[0,1] neg_hi:[0,1]
	v_pk_mul_f32 v[122:123], v[18:19], s[2:3]
	v_pk_mul_f32 v[40:41], v[46:47], v[38:39] op_sel:[0,1] op_sel_hi:[1,0] neg_lo:[0,1]
	v_pk_fma_f32 v[122:123], v[16:17], s[78:79], v[122:123]
	v_pk_fma_f32 v[96:97], v[48:49], v[38:39], v[40:41]
	v_pk_add_f32 v[38:39], v[90:91], v[94:95]
	v_pk_add_f32 v[40:41], v[92:93], v[96:97]
	s_mov_b64 s[2:3], -1
	v_pk_add_f32 v[116:117], v[38:39], v[40:41]
	s_and_b64 vcc, exec, s[4:5]
	v_pk_mul_f32 v[116:117], v[122:123], v[116:117]
	s_nop 0
	v_mul_f32_e32 v44, v13, v44
	v_add_f32_e32 v10, v116, v10
	v_add_f32_e32 v10, v117, v10
	v_fmac_f32_e32 v44, v194, v10
	v_mul_f32_e32 v10, v15, v44
	s_cbranch_vccnz .LBB0_2776
	v_bfe_u32 v15, v10, 16, 1
	v_add3_u32 v15, v10, v15, s33
	v_lshl_add_u64 v[42:43], v[42:43], 1, s[54:55]
	s_mov_b64 s[2:3], 0
	global_store_short_d16_hi v[42:43], v15, off

.LBB0_2782:
	s_or_b64 exec, exec, s[2:3]
	v_pk_add_f32 v[42:43], v[100:101], v[108:109] neg_lo:[0,1] neg_hi:[0,1]
	v_pk_add_f32 v[98:99], v[98:99], v[106:107] neg_lo:[0,1] neg_hi:[0,1]
	v_pk_mul_f32 v[44:45], v[46:47], v[42:43] op_sel:[0,1] op_sel_hi:[1,0] neg_lo:[0,1]
	s_mov_b32 s2, s81
	v_pk_fma_f32 v[100:101], v[46:47], v[42:43], v[44:45]
	v_pk_add_f32 v[42:43], v[102:103], v[110:111] neg_lo:[0,1] neg_hi:[0,1]
	s_mov_b32 s3, s80
	v_xor_b32_e32 v102, 0x80000000, v43
	v_mov_b32_e32 v103, v42
	v_pk_add_f32 v[42:43], v[104:105], v[112:113] neg_lo:[0,1] neg_hi:[0,1]
	v_pk_mul_f32 v[108:109], v[18:19], s[2:3]
	v_pk_mul_f32 v[44:45], v[46:47], v[42:43] op_sel:[0,1] op_sel_hi:[1,0] neg_lo:[0,1]
	v_pk_fma_f32 v[108:109], v[16:17], s[80:81], v[108:109]
	v_pk_fma_f32 v[104:105], v[48:49], v[42:43], v[44:45]
	v_pk_add_f32 v[42:43], v[98:99], v[102:103]
	v_pk_add_f32 v[44:45], v[100:101], v[104:105]
	s_mov_b64 s[2:3], -1
	v_pk_add_f32 v[106:107], v[42:43], v[44:45]
	s_nop 0
	v_pk_mul_f32 v[106:107], v[108:109], v[106:107]
	s_nop 0
	v_add_f32_e32 v10, v106, v10
	s_nop 0
	v_lshlrev_b32_e32 v106, 16, v123
	v_mul_f32_e32 v106, v191, v106
	v_fmac_f32_e32 v106, v189, v122
	v_fmac_f32_e32 v106, v192, v15
	v_add_f32_e32 v15, v193, v106
	v_add_co_u32_e32 v106, vcc, 0x3000, v2
	v_add_f32_e32 v10, v107, v10
	s_nop 0
	v_addc_co_u32_e32 v107, vcc, 0, v3, vcc
	v_mov_b32_e32 v106, v228
	s_and_b64 vcc, exec, s[4:5]
	s_nop 0
	v_mul_f32_e32 v106, v13, v106
	v_fmac_f32_e32 v106, v194, v10
	v_mul_f32_e32 v10, v15, v106
	s_cbranch_vccnz .LBB0_2784
	v_bfe_u32 v15, v10, 16, 1
	v_add3_u32 v15, v10, v15, s33
	v_lshl_add_u64 v[106:107], v[116:117], 1, s[54:55]
	s_mov_b64 s[2:3], 0
	global_store_short_d16_hi v[106:107], v15, off

.LBB0_2790:
	s_or_b64 exec, exec, s[2:3]
	v_pk_add_f32 v[108:109], v[118:119], v[132:133] neg_lo:[0,1] neg_hi:[0,1]
	v_pk_add_f32 v[112:113], v[120:121], v[134:135] neg_lo:[0,1] neg_hi:[0,1]
	v_pk_mul_f32 v[110:111], v[46:47], v[108:109] op_sel:[0,1] op_sel_hi:[1,0] neg_lo:[0,1]
	v_pk_add_f32 v[106:107], v[114:115], v[130:131] neg_lo:[0,1] neg_hi:[0,1]
	v_pk_fma_f32 v[108:109], v[46:47], v[108:109], v[110:111]
	v_xor_b32_e32 v110, 0x80000000, v113
	v_mov_b32_e32 v111, v112
	v_pk_add_f32 v[112:113], v[124:125], v[136:137] neg_lo:[0,1] neg_hi:[0,1]
	s_mov_b32 s2, s9
	v_pk_mul_f32 v[46:47], v[46:47], v[112:113] op_sel:[0,1] op_sel_hi:[1,0] neg_lo:[0,1]
	s_mov_b32 s3, s8
	v_pk_fma_f32 v[112:113], v[48:49], v[112:113], v[46:47]
	v_pk_add_f32 v[46:47], v[106:107], v[110:111]
	v_pk_add_f32 v[48:49], v[108:109], v[112:113]
	v_pk_mul_f32 v[118:119], v[18:19], s[2:3]
	v_pk_add_f32 v[114:115], v[46:47], v[48:49]
	v_pk_fma_f32 v[118:119], v[16:17], s[8:9], v[118:119]
	s_mov_b64 s[2:3], -1
	v_pk_mul_f32 v[114:115], v[118:119], v[114:115]
	s_nop 0
	v_add_f32_e32 v10, v114, v10
	s_nop 0
	v_lshlrev_b32_e32 v114, 16, v123
	v_mul_f32_e32 v114, v191, v114
	v_fmac_f32_e32 v114, v189, v122
	v_fmac_f32_e32 v114, v192, v15
	v_add_f32_e32 v15, v193, v114
	v_add_co_u32_e32 v114, vcc, 0x3000, v2
	v_add_f32_e32 v10, v115, v10
	s_nop 0
	v_addc_co_u32_e32 v115, vcc, 0, v3, vcc
	v_mov_b32_e32 v114, v233
	s_and_b64 vcc, exec, s[4:5]
	s_nop 0
	v_mul_f32_e32 v114, v13, v114
	v_fmac_f32_e32 v114, v194, v10
	v_mul_f32_e32 v10, v15, v114
	s_cbranch_vccnz .LBB0_2792
	v_bfe_u32 v15, v10, 16, 1
	v_add3_u32 v15, v10, v15, s33
	v_lshl_add_u64 v[114:115], v[116:117], 1, s[54:55]
	s_mov_b64 s[2:3], 0
	global_store_short_d16_hi v[114:115], v15, off
